# layer-1 w_down, w_out and a quarter of w_up transposed in the layer-1 in-projection idle slot (65 region steps per idle workgroup)
# baseline (speedup 1.0000x reference)
; #define GAS __attribute__((address_space(1)))
; #define LAS __attribute__((address_space(3)))
; #define LDS_WAIT() asm volatile("s_waitcnt lgkmcnt(0)" ::: "memory")
; __device__ __forceinline__ int nat_dim(int p) { return (p >> 1) + 64 * (p & 1); }
; template <int MAP, bool KS, bool KPERM = false>
; __device__ __forceinline__ void p0_transpose_item(const float* W, int K, int Nsrc, int nblk, bf16* WT, const float* ksA, const float* ksB, int ksplit, LAS float* scr, int item, int lane) {
;     const int kb = item / nblk, nb = item % nblk, k0 = 64 * kb, n0 = 32 * nb;
;     const int nr = n0 + (lane & 31); const int sc = MAP == 1 ? src_col_in(nr) : (MAP == 2 ? nat_dim(nr) : nr);
;     float v[32];
; #pragma unroll
;     for (int i = 0; i < 32; ++i) { const int k = k0 + 2 * i + (lane >> 5); const int ksrc = KPERM ? ((k & ~127) + nat_dim(k & 127)) : k;
;         v[i] = sc >= 0 ? W[(size_t)ksrc * Nsrc + sc] : 0.f; }
; #pragma unroll
;     for (int i = 0; i < 32; ++i) { const int kk = 2 * i + (lane >> 5); const int k = k0 + kk;
;         if (KS) v[i] *= (k < ksplit ? ksA[k] : ksB[k - ksplit]);
;         scr[kk * 33 + (lane & 31)] = v[i]; }
;     LDS_WAIT(); asm volatile("" ::: "memory");
;     const int c = lane & 7;
; #pragma unroll
;     for (int j = 0; j < 4; ++j) { const int n = (lane >> 3) + 8 * j; const LAS float* s = scr + (8 * c) * 33 + n;
;         v4u o; o.x = pk2(s[0 * 33], s[1 * 33]); o.y = pk2(s[2 * 33], s[3 * 33]); o.z = pk2(s[4 * 33], s[5 * 33]); o.w = pk2(s[6 * 33], s[7 * 33]);
;         *(GAS v4u*)(WT + (size_t)(n0 + n) * K + k0 + 8 * c) = o; }
; __global__ void __launch_bounds__(NWAVES * 64, 2) hybrid_fwd(Args args) {
;     ...
;     {
;         PHASE_IDS();
;         LAS float* scr = (LAS float*)(F.lds + RING_OFF + wave * 16384);
;         constexpr int I_IN = (DM / 64) * (NPROJ / 32), I_O = (DM / 64) * (DM / 32), I_UP = (DM / 64) * (FF / 32), I_DN = (FF / 64) * (DM / 32);
;         constexpr int I_L = I_IN + I_O + I_UP + I_DN;
;         for (int rep = 0; rep < REP_PRO; ++rep)
;         for (int it = gw; it < DEPTH * I_L; it += NGW) {
;             const int l = it / I_L; int r = it % I_L;
;             if (r < I_IN) { if (l >= PROJ_F8_FROM) p0_transpose_item_f8<true, 1>(args.in[2] + (size_t)l * DM * NSRC, DM, NSRC, NPROJ / 32, (unsigned char*)(ws + WS_WIN + l * SZ_WIN), WUP8_SCALE, args.in[1] + l * DM, args.in[1] + l * DM, DM, scr, r, lane);
.LBB0_11:
	s_or_b64 exec, exec, s[0:1]
	v_mov_b32_e32 v1, v0
	v_readlane_b32 s1, v253, 2
	v_readfirstlane_b32 s0, v1
	s_ashr_i32 s0, s0, 6
	s_lshl_b32 s1, s1, 3
	s_add_i32 s80, s0, s1
	s_lshl_b32 s0, s0, 14
	v_lshlrev_b32_e32 v2, 3, v1
	v_writelane_b32 v253, s1, 46
	s_add_i32 s1, s0, 0
	v_and_b32_e32 v18, 31, v1
	v_bfe_u32 v20, v1, 3, 3
	v_and_b32_e32 v8, 56, v2
	s_lshl_b32 s96, s83, 3
	s_lshl_b32 s76, s83, 9
	v_bfe_u32 v6, v1, 5, 1
	v_lshl_add_u32 v25, v18, 2, s1
	s_movk_i32 s0, 0x84
	v_mul_u32_u24_e32 v2, 0x84, v8
	v_lshlrev_b32_e32 v3, 2, v20
	s_cmp_gt_i32 s80, 0x2f3ff
	v_mad_u32_u24 v19, v6, s0, v25
	v_mov_b32_e32 v11, 0
	v_add3_u32 v21, s1, v2, v3
	v_or_b32_e32 v22, 8, v20
	v_or_b32_e32 v23, 16, v20
	v_or_b32_e32 v24, 24, v20
	s_cbranch_scc1 .Lco3_hop_192
	v_and_b32_e32 v249, 63, v0
	v_lshrrev_b32_e32 v250, 6, v0
	v_readlane_b32 s15, v253, 2
	s_lshr_b32 s22, s15, 3
	s_and_b32 s23, s15, 7
	v_lshrrev_b32_e32 v246, 5, v249
	v_lshl_add_u32 v247, v250, 4, v246
	v_and_b32_e32 v248, 31, v249
	v_xor_b32_e32 v248, v248, v250
	v_lshlrev_b32_e32 v248, 4, v248
	v_lshl_add_u32 v209, v247, 9, v248
	v_add_u32_e32 v210, 0x10000, v209
	v_lshlrev_b32_e32 v96, 2, v247
	v_and_b32_e32 v248, 31, v249
	v_lshlrev_b32_e32 v248, 4, v248
	s_mov_b32 s20, 0x10000
	v_mad_u32_u24 v74, v247, s20, v248
	s_mov_b32 s20, 0x4000
	v_mad_u32_u24 v75, v247, s20, v248
	s_mov_b32 s20, 0xb140
	v_mad_u32_u24 v76, v247, s20, v248
	v_and_b32_e32 v246, 7, v249
	v_lshrrev_b32_e32 v247, 5, v249
	v_lshl_add_u32 v247, v250, 2, v247
	v_xor_b32_e32 v247, v247, v246
	v_lshlrev_b32_e32 v247, 4, v247
	v_lshl_add_u32 v247, v246, 13, v247
	v_bfe_u32 v248, v249, 3, 2
	v_lshl_add_u32 v211, v248, 2, v247
	v_add_u32_e32 v212, 0x10000, v211
	v_and_b32_e32 v246, 7, v249
	v_lshrrev_b32_e32 v247, 5, v249
	v_lshl_add_u32 v247, v250, 2, v247
	v_add_u32_e32 v247, 2, v247
	v_xor_b32_e32 v247, v247, v246
	v_lshlrev_b32_e32 v247, 4, v247
	v_lshl_add_u32 v247, v246, 13, v247
	v_bfe_u32 v248, v249, 3, 2
	v_lshl_add_u32 v213, v248, 2, v247
	v_add_u32_e32 v214, 0x10000, v213
	v_and_b32_e32 v246, 15, v249
	v_lshrrev_b32_e32 v247, 1, v246
	v_lshlrev_b32_e32 v248, 2, v250
	v_xor_b32_e32 v248, v248, v247
	v_lshlrev_b32_e32 v248, 4, v248
	v_lshl_add_u32 v248, v246, 12, v248
	v_lshrrev_b32_e32 v247, 4, v249
	v_lshl_add_u32 v112, v247, 2, v248
	v_add_u32_e32 v113, 0x10000, v112
	v_and_b32_e32 v246, 15, v249
	v_lshrrev_b32_e32 v247, 1, v246
	v_lshlrev_b32_e32 v248, 2, v250
	v_add_u32_e32 v248, 1, v248
	v_xor_b32_e32 v248, v248, v247
	v_lshlrev_b32_e32 v248, 4, v248
	v_lshl_add_u32 v248, v246, 12, v248
	v_lshrrev_b32_e32 v247, 4, v249
	v_lshl_add_u32 v114, v247, 2, v248
	v_add_u32_e32 v115, 0x10000, v114
	v_and_b32_e32 v246, 15, v249
	v_lshrrev_b32_e32 v247, 1, v246
	v_lshlrev_b32_e32 v248, 2, v250
	v_add_u32_e32 v248, 2, v248
	v_xor_b32_e32 v248, v248, v247
	v_lshlrev_b32_e32 v248, 4, v248
	v_lshl_add_u32 v248, v246, 12, v248
	v_lshrrev_b32_e32 v247, 4, v249
	v_lshl_add_u32 v116, v247, 2, v248
	v_add_u32_e32 v117, 0x10000, v116
	v_and_b32_e32 v246, 15, v249
	v_lshrrev_b32_e32 v247, 1, v246
	v_lshlrev_b32_e32 v248, 2, v250
	v_add_u32_e32 v248, 3, v248
	v_xor_b32_e32 v248, v248, v247
	v_lshlrev_b32_e32 v248, 4, v248
	v_lshl_add_u32 v248, v246, 12, v248
	v_lshrrev_b32_e32 v247, 4, v249
	v_lshl_add_u32 v118, v247, 2, v248
	v_add_u32_e32 v119, 0x10000, v118
	v_lshrrev_b32_e32 v246, 3, v249
	v_lshl_add_u32 v246, v250, 4, v246
	v_and_b32_e32 v247, 7, v249
	v_lshlrev_b32_e32 v247, 4, v247
	v_lshl_add_u32 v77, v246, 12, v247
	v_lshl_add_u32 v79, v246, 14, v247
	v_and_b32_e32 v248, 63, v246
	v_lshlrev_b32_e32 v248, 1, v248
	v_lshrrev_b32_e32 v246, 6, v246
	v_or_b32_e32 v248, v248, v246
	v_lshl_add_u32 v81, v248, 12, v247
	v_lshrrev_b32_e32 v246, 3, v249
	v_lshl_add_u32 v246, v250, 4, v246
	v_add_u32_e32 v246, 8, v246
	v_and_b32_e32 v247, 7, v249
	v_lshlrev_b32_e32 v247, 4, v247
	v_lshl_add_u32 v78, v246, 12, v247
	v_lshl_add_u32 v80, v246, 14, v247
	v_and_b32_e32 v248, 63, v246
	v_lshlrev_b32_e32 v248, 1, v248
	v_lshrrev_b32_e32 v246, 6, v246
	v_or_b32_e32 v248, v248, v246
	v_lshl_add_u32 v82, v248, 12, v247
	v_lshrrev_b32_e32 v246, 4, v249
	v_lshl_add_u32 v246, v250, 4, v246
	v_and_b32_e32 v247, 15, v249
	v_lshlrev_b32_e32 v247, 4, v247
	v_lshl_add_u32 v83, v246, 13, v247
	v_and_b32_e32 v248, 63, v246
	v_lshlrev_b32_e32 v248, 1, v248
	v_lshrrev_b32_e32 v246, 6, v246
	v_or_b32_e32 v248, v248, v246
	v_lshl_add_u32 v87, v248, 13, v247
	v_lshrrev_b32_e32 v246, 4, v249
	v_lshl_add_u32 v246, v250, 4, v246
	v_add_u32_e32 v246, 4, v246
	v_and_b32_e32 v247, 15, v249
	v_lshlrev_b32_e32 v247, 4, v247
	v_lshl_add_u32 v84, v246, 13, v247
	v_and_b32_e32 v248, 63, v246
	v_lshlrev_b32_e32 v248, 1, v248
	v_lshrrev_b32_e32 v246, 6, v246
	v_or_b32_e32 v248, v248, v246
	v_lshl_add_u32 v88, v248, 13, v247
	v_lshrrev_b32_e32 v246, 4, v249
	v_lshl_add_u32 v246, v250, 4, v246
	v_add_u32_e32 v246, 8, v246
	v_and_b32_e32 v247, 15, v249
	v_lshlrev_b32_e32 v247, 4, v247
	v_lshl_add_u32 v85, v246, 13, v247
	v_and_b32_e32 v248, 63, v246
	v_lshlrev_b32_e32 v248, 1, v248
	v_lshrrev_b32_e32 v246, 6, v246
	v_or_b32_e32 v248, v248, v246
	v_lshl_add_u32 v89, v248, 13, v247
	v_lshrrev_b32_e32 v246, 4, v249
	v_lshl_add_u32 v246, v250, 4, v246
	v_add_u32_e32 v246, 12, v246
	v_and_b32_e32 v247, 15, v249
	v_lshlrev_b32_e32 v247, 4, v247
	v_lshl_add_u32 v86, v246, 13, v247
	v_and_b32_e32 v248, 63, v246
	v_lshlrev_b32_e32 v248, 1, v248
	v_lshrrev_b32_e32 v246, 6, v246
	v_or_b32_e32 v248, v248, v246
	v_lshl_add_u32 v90, v248, 13, v247
	v_mov_b32_e32 v95, 0x43e00000
	s_mov_b32 s62, 0xc3e00000
	s_mov_b32 s63, 0x7fff
	s_mov_b32 s64, 0x07060302
	v_readlane_b32 s10, v253, 5
;     ...
;     for (int i = 0; i < 32; ++i) v[i] = sc >= 0 ? W[(size_t)(k0 + 2 * i + (lane >> 5)) * Nsrc + sc] : 0.f;
; #pragma unroll
;     for (int i = 0; i < 32; ++i) { const int k = k0 + 2 * i + (lane >> 5); float x = v[i] * wscale; if (KS) x *= (k < ksplit ? ksA[k] : ksB[k - ksplit]); scr[(2 * i + (lane >> 5)) * 33 + (lane & 31)] = x; }
; __global__ void __launch_bounds__(NWAVES * 64, 2) hybrid_fwd(Args args) {
;     ...
;             if (r < I_IN) { if (l >= PROJ_F8_FROM) p0_transpose_item_f8<true, 1>(args.in[2] + (size_t)l * DM * NSRC, DM, NSRC, NPROJ / 32, (unsigned char*)(ws + WS_WIN + l * SZ_WIN), WUP8_SCALE, args.in[1] + l * DM, args.in[1] + l * DM, DM, scr, r, lane);
;                 else p0_transpose_item<1, true>(args.in[2] + (size_t)l * DM * NSRC, DM, NSRC, NPROJ / 32, (bf16*)(ws + WS_WIN + l * SZ_WIN), args.in[1] + l * DM, args.in[1] + l * DM, DM, scr, r, lane); continue; } r -= I_IN;
;             if (r < I_O) { if (l >= WO_F8_FROM) p0_transpose_item_f8<true>(args.in[13] + (size_t)l * DM * DM, DM, DM, DM / 32, (unsigned char*)(ws + WS_WO + l * SZ_WO), 64.f, args.in[6] + l * 2048, args.in[12] + l * 2048, 2048, scr, r, lane);
;                 else p0_transpose_item<0, true>(args.in[13] + (size_t)l * DM * DM, DM, DM, DM / 32, (bf16*)(ws + WS_WO + l * SZ_WO), args.in[6] + l * 2048, args.in[12] + l * 2048, 2048, scr, r, lane); continue; } r -= I_O;
;             if (r < I_UP) { p0_transpose_item_f8<true>(args.in[15] + (size_t)l * DM * FF, DM, FF, FF / 32, (unsigned char*)(ws + WS_WUP + l * SZ_WUP), WUP8_SCALE, args.in[14] + l * DM, args.in[14] + l * DM, DM, scr, r, lane); continue; } r -= I_UP;
	v_readlane_b32 s11, v253, 6
	s_lshl_b32 s20, s22, 9
	s_add_u32 s10, s10, s20
	s_addc_u32 s11, s11, 0
	global_load_dword v42, v96, s[10:11] offset:0
	global_load_dword v43, v96, s[10:11] offset:8
	global_load_dword v44, v96, s[10:11] offset:16
	global_load_dword v45, v96, s[10:11] offset:24
	global_load_dword v46, v96, s[10:11] offset:32
	global_load_dword v47, v96, s[10:11] offset:40
	global_load_dword v48, v96, s[10:11] offset:48
	global_load_dword v49, v96, s[10:11] offset:56
	v_readlane_b32 s10, v253, 5
	v_readlane_b32 s11, v253, 6
	s_lshl_b32 s20, s22, 9
	s_add_i32 s20, s20, 0x4000
	s_add_u32 s10, s10, s20
	s_addc_u32 s11, s11, 0
	global_load_dword v50, v96, s[10:11] offset:0
	global_load_dword v51, v96, s[10:11] offset:8
	global_load_dword v52, v96, s[10:11] offset:16
	global_load_dword v53, v96, s[10:11] offset:24
	global_load_dword v54, v96, s[10:11] offset:32
	global_load_dword v55, v96, s[10:11] offset:40
	global_load_dword v56, v96, s[10:11] offset:48
	global_load_dword v57, v96, s[10:11] offset:56
	v_readlane_b32 s10, v253, 15
	v_readlane_b32 s11, v253, 16
	v_readlane_b32 s20, v253, 27
	v_readlane_b32 s21, v253, 28
	s_sub_i32 s26, s22, 16
	s_cmp_lt_u32 s22, 16
	s_cselect_b32 s10, s10, s20
	s_cselect_b32 s11, s11, s21
	s_cselect_b32 s26, s22, s26
	s_lshl_b32 s20, s26, 9
	s_add_u32 s10, s10, s20
	s_addc_u32 s11, s11, 0
	global_load_dword v58, v96, s[10:11] offset:0
	global_load_dword v59, v96, s[10:11] offset:8
	global_load_dword v60, v96, s[10:11] offset:16
	global_load_dword v61, v96, s[10:11] offset:24
	global_load_dword v62, v96, s[10:11] offset:32
	global_load_dword v63, v96, s[10:11] offset:40
	global_load_dword v64, v96, s[10:11] offset:48
	global_load_dword v65, v96, s[10:11] offset:56
	v_readlane_b32 s10, v253, 15
	v_readlane_b32 s11, v253, 16
	v_readlane_b32 s20, v253, 27
	v_readlane_b32 s21, v253, 28
	s_sub_i32 s26, s22, 16
	s_cmp_lt_u32 s22, 16
	s_cselect_b32 s10, s10, s20
	s_cselect_b32 s11, s11, s21
	s_cselect_b32 s26, s22, s26
	s_lshl_b32 s20, s26, 9
	s_add_i32 s20, s20, 0x2000
	s_add_u32 s10, s10, s20
	s_addc_u32 s11, s11, 0
	global_load_dword v66, v96, s[10:11] offset:0
	global_load_dword v67, v96, s[10:11] offset:8
	global_load_dword v68, v96, s[10:11] offset:16
	global_load_dword v69, v96, s[10:11] offset:24
	global_load_dword v70, v96, s[10:11] offset:32
	global_load_dword v71, v96, s[10:11] offset:40
	global_load_dword v72, v96, s[10:11] offset:48
	global_load_dword v73, v96, s[10:11] offset:56
	v_readlane_b32 s10, v253, 31
	v_readlane_b32 s11, v253, 32
	s_lshl_b32 s20, s22, 9
	s_add_u32 s10, s10, s20
	s_addc_u32 s11, s11, 0
	global_load_dword v26, v96, s[10:11] offset:0
	global_load_dword v27, v96, s[10:11] offset:8
	global_load_dword v28, v96, s[10:11] offset:16
	global_load_dword v29, v96, s[10:11] offset:24
	global_load_dword v30, v96, s[10:11] offset:32
	global_load_dword v31, v96, s[10:11] offset:40
	global_load_dword v32, v96, s[10:11] offset:48
	global_load_dword v33, v96, s[10:11] offset:56
	v_readlane_b32 s10, v253, 31
	v_readlane_b32 s11, v253, 32
	s_lshl_b32 s20, s22, 9
	s_add_i32 s20, s20, 0x4000
	s_add_u32 s10, s10, s20
	s_addc_u32 s11, s11, 0
	global_load_dword v34, v96, s[10:11] offset:0
	global_load_dword v35, v96, s[10:11] offset:8
	global_load_dword v36, v96, s[10:11] offset:16
	global_load_dword v37, v96, s[10:11] offset:24
	global_load_dword v38, v96, s[10:11] offset:32
	global_load_dword v39, v96, s[10:11] offset:40
	global_load_dword v40, v96, s[10:11] offset:48
	global_load_dword v41, v96, s[10:11] offset:56
	s_waitcnt vmcnt(0)
	v_mul_f32_e32 v50, 0x42800000, v50
	v_mul_f32_e32 v51, 0x42800000, v51
	v_mul_f32_e32 v52, 0x42800000, v52
	v_mul_f32_e32 v53, 0x42800000, v53
	v_mul_f32_e32 v54, 0x42800000, v54
	v_mul_f32_e32 v55, 0x42800000, v55
	v_mul_f32_e32 v56, 0x42800000, v56
	v_mul_f32_e32 v57, 0x42800000, v57
	v_mul_f32_e32 v66, 0x42800000, v66
	v_mul_f32_e32 v67, 0x42800000, v67
	v_mul_f32_e32 v68, 0x42800000, v68
	v_mul_f32_e32 v69, 0x42800000, v69
	v_mul_f32_e32 v70, 0x42800000, v70
	v_mul_f32_e32 v71, 0x42800000, v71
	v_mul_f32_e32 v72, 0x42800000, v72
	v_mul_f32_e32 v73, 0x42800000, v73
	v_mul_f32_e32 v26, 0x42800000, v26
	v_mul_f32_e32 v27, 0x42800000, v27
	v_mul_f32_e32 v28, 0x42800000, v28
	v_mul_f32_e32 v29, 0x42800000, v29
	v_mul_f32_e32 v30, 0x42800000, v30
	v_mul_f32_e32 v31, 0x42800000, v31
	v_mul_f32_e32 v32, 0x42800000, v32
	v_mul_f32_e32 v33, 0x42800000, v33
	v_mul_f32_e32 v34, 0x42800000, v34
	v_mul_f32_e32 v35, 0x42800000, v35
	v_mul_f32_e32 v36, 0x42800000, v36
	v_mul_f32_e32 v37, 0x42800000, v37
	v_mul_f32_e32 v38, 0x42800000, v38
	v_mul_f32_e32 v39, 0x42800000, v39
	v_mul_f32_e32 v40, 0x42800000, v40
	v_mul_f32_e32 v41, 0x42800000, v41
	v_readlane_b32 s30, v253, 33
	v_readlane_b32 s31, v253, 34
	v_readlane_b32 s32, v253, 41
	v_readlane_b32 s33, v253, 42
	s_mul_i32 s20, s22, 0x800000
	s_lshl_b32 s21, s23, 9
	s_add_u32 s20, s20, s21
	s_add_u32 s30, s30, s20
	s_addc_u32 s31, s31, 0
	s_add_u32 s32, s32, 0xf600000
	s_addc_u32 s33, s33, 0
	s_lshl_b32 s20, s22, 7
	s_mul_i32 s21, s23, 0x80000
	s_add_u32 s20, s20, s21
	s_add_u32 s32, s32, s20
	s_addc_u32 s33, s33, 0
	v_readlane_b32 s34, v253, 33
	v_readlane_b32 s35, v253, 34
	v_readlane_b32 s36, v253, 41
	v_readlane_b32 s37, v253, 42
	s_add_u32 s34, s34, 0x10000000
	s_addc_u32 s35, s35, 0
	s_mul_i32 s20, s22, 0x800000
	s_lshl_b32 s21, s23, 9
	s_add_u32 s20, s20, s21
	s_add_u32 s34, s34, s20
	s_addc_u32 s35, s35, 0
	s_add_u32 s36, s36, 0x17600000
	s_addc_u32 s37, s37, 0
	s_lshl_b32 s20, s22, 7
	s_mul_i32 s21, s23, 0x80000
	s_add_u32 s20, s20, s21
	s_add_u32 s36, s36, s20
	s_addc_u32 s37, s37, 0
	v_readlane_b32 s38, v253, 35
;     const int pr = item >> 1, kb = 2 * (pr / nblk) + (item & 1), nb = pr % nblk, k0 = 64 * kb, n0 = 32 * nb;
;     const int nr = n0 + (lane & 31); const int sc = MAP == 1 ? src_col_in(nr) : nr;
;     float v[32];
; #pragma unroll
;     for (int i = 0; i < 32; ++i) v[i] = sc >= 0 ? W[(size_t)(k0 + 2 * i + (lane >> 5)) * Nsrc + sc] : 0.f;
; #pragma unroll
;     for (int i = 0; i < 32; ++i) { const int k = k0 + 2 * i + (lane >> 5); float x = v[i] * wscale; if (KS) x *= (k < ksplit ? ksA[k] : ksB[k - ksplit]); scr[(2 * i + (lane >> 5)) * 33 + (lane & 31)] = x; }
; __global__ void __launch_bounds__(NWAVES * 64, 2) hybrid_fwd(Args args) {
;     ...
;             if (r < I_UP) { p0_transpose_item_f8<true>(args.in[15] + (size_t)l * DM * FF, DM, FF, FF / 32, (unsigned char*)(ws + WS_WUP + l * SZ_WUP), WUP8_SCALE, args.in[14] + l * DM, args.in[14] + l * DM, DM, scr, r, lane); continue; } r -= I_UP;
	v_readlane_b32 s39, v253, 36
	v_readlane_b32 s40, v253, 41
	v_readlane_b32 s41, v253, 42
	s_mul_i32 s20, s22, 0x200000
	s_lshl_b32 s21, s23, 9
	s_add_u32 s20, s20, s21
	s_add_u32 s38, s38, s20
	s_addc_u32 s39, s39, 0
	s_add_u32 s40, s40, 0x1f600000
	s_addc_u32 s41, s41, 0
	s_lshl_b32 s20, s22, 7
	s_mul_i32 s21, s23, 0x200000
	s_add_u32 s20, s20, s21
	s_add_u32 s40, s40, s20
	s_addc_u32 s41, s41, 0
	v_readlane_b32 s42, v253, 35
	v_readlane_b32 s43, v253, 36
	v_readlane_b32 s44, v253, 41
	v_readlane_b32 s45, v253, 42
	s_add_u32 s42, s42, 0x10000000
	s_addc_u32 s43, s43, 0
	s_mul_i32 s20, s22, 0x200000
	s_lshl_b32 s21, s23, 9
	s_add_u32 s20, s20, s21
	s_add_u32 s42, s42, s20
	s_addc_u32 s43, s43, 0
	s_add_u32 s44, s44, 0x27600000
	s_addc_u32 s45, s45, 0
	s_lshl_b32 s20, s22, 7
	s_mul_i32 s21, s23, 0x200000
	s_add_u32 s20, s20, s21
	s_add_u32 s44, s44, s20
	s_addc_u32 s45, s45, 0
	v_readlane_b32 s46, v253, 7
	v_readlane_b32 s47, v253, 8
	v_readlane_b32 s48, v253, 41
	v_readlane_b32 s49, v253, 42
	s_mul_i32 s20, s22, 0x58a000
	s_add_u32 s46, s46, s20
	s_addc_u32 s47, s47, 0
	s_add_u32 s48, s48, 0x200000
	s_addc_u32 s49, s49, 0
	s_lshl_b32 s20, s22, 8
	s_add_u32 s48, s48, s20
	s_addc_u32 s49, s49, 0
	v_readlane_b32 s50, v253, 7
	v_readlane_b32 s51, v253, 8
	v_readlane_b32 s52, v253, 41
	v_readlane_b32 s53, v253, 42
	s_add_u32 s50, s50, 0xb140000
	s_addc_u32 s51, s51, 0
	s_mul_i32 s20, s22, 0x58a000
	s_add_u32 s50, s50, s20
	s_addc_u32 s51, s51, 0
	s_add_u32 s52, s52, 0x5c00000
	s_addc_u32 s53, s53, 0
	s_lshl_b32 s20, s22, 7
	s_add_u32 s52, s52, s20
	s_addc_u32 s53, s53, 0
	v_readlane_b32 s54, v253, 29
	v_readlane_b32 s55, v253, 30
	v_readlane_b32 s56, v253, 41
	v_readlane_b32 s57, v253, 42
	s_mul_i32 s20, s22, 0x200000
	s_lshl_b32 s21, s23, 9
	s_add_u32 s20, s20, s21
	s_add_u32 s54, s54, s20
	s_addc_u32 s55, s55, 0
	s_add_u32 s56, s56, 0xb600000
	s_addc_u32 s57, s57, 0
	s_lshl_b32 s20, s22, 8
	s_mul_i32 s21, s23, 0x100000
	s_add_u32 s20, s20, s21
	s_add_u32 s56, s56, s20
	s_addc_u32 s57, s57, 0
	v_readlane_b32 s58, v253, 29
	v_readlane_b32 s59, v253, 30
	v_readlane_b32 s60, v253, 41
	v_readlane_b32 s61, v253, 42
	s_add_u32 s58, s58, 0x4000000
	s_addc_u32 s59, s59, 0
	s_mul_i32 s20, s22, 0x200000
	s_lshl_b32 s21, s23, 9
	s_add_u32 s20, s20, s21
	s_add_u32 s58, s58, s20
	s_addc_u32 s59, s59, 0
	s_add_u32 s60, s60, 0xd600000
	s_addc_u32 s61, s61, 0
	s_lshl_b32 s20, s22, 7
	s_mul_i32 s21, s23, 0x80000
	s_add_u32 s20, s20, s21
	s_add_u32 s60, s60, s20
	s_addc_u32 s61, s61, 0
	s_mov_b64 s[8:9], s[30:31]
	global_load_dwordx4 v[144:147], v74, s[8:9]
	s_add_u32 s8, s8, 0x20000
	s_addc_u32 s9, s9, 0
	global_load_dwordx4 v[148:151], v74, s[8:9]
	s_add_u32 s8, s8, 0x20000
	s_addc_u32 s9, s9, 0
	global_load_dwordx4 v[152:155], v74, s[8:9]
	s_add_u32 s8, s8, 0x20000
	s_addc_u32 s9, s9, 0
	global_load_dwordx4 v[156:159], v74, s[8:9]
	s_add_u32 s8, s8, 0x20000
	s_addc_u32 s9, s9, 0
	global_load_dwordx4 v[160:163], v74, s[8:9]
	s_add_u32 s8, s8, 0x20000
	s_addc_u32 s9, s9, 0
	global_load_dwordx4 v[164:167], v74, s[8:9]
	s_add_u32 s8, s8, 0x20000
	s_addc_u32 s9, s9, 0
	global_load_dwordx4 v[168:171], v74, s[8:9]
	s_add_u32 s8, s8, 0x20000
	s_addc_u32 s9, s9, 0
	global_load_dwordx4 v[172:175], v74, s[8:9]
	s_add_u32 s8, s30, 0x1000
	s_addc_u32 s9, s31, 0
	global_load_dwordx4 v[176:179], v74, s[8:9]
	s_add_u32 s8, s8, 0x20000
	s_addc_u32 s9, s9, 0
	global_load_dwordx4 v[180:183], v74, s[8:9]
	s_add_u32 s8, s8, 0x20000
	s_addc_u32 s9, s9, 0
	global_load_dwordx4 v[184:187], v74, s[8:9]
	s_add_u32 s8, s8, 0x20000
	s_addc_u32 s9, s9, 0
	global_load_dwordx4 v[188:191], v74, s[8:9]
	s_add_u32 s8, s8, 0x20000
	s_addc_u32 s9, s9, 0
	global_load_dwordx4 v[192:195], v74, s[8:9]
	s_add_u32 s8, s8, 0x20000
	s_addc_u32 s9, s9, 0
	global_load_dwordx4 v[196:199], v74, s[8:9]
	s_add_u32 s8, s8, 0x20000
	s_addc_u32 s9, s9, 0
	global_load_dwordx4 v[200:203], v74, s[8:9]
	s_add_u32 s8, s8, 0x20000
	s_addc_u32 s9, s9, 0
	global_load_dwordx4 v[204:207], v74, s[8:9]
	s_waitcnt vmcnt(8)
	v_mul_f32_e32 v144, v26, v144
	v_mul_f32_e32 v145, v26, v145
	v_mul_f32_e32 v146, v26, v146
	v_mul_f32_e32 v147, v26, v147
	ds_write_b128 v209, v[144:147]
	v_mul_f32_e32 v148, v27, v148
	v_mul_f32_e32 v149, v27, v149
	v_mul_f32_e32 v150, v27, v150
	v_mul_f32_e32 v151, v27, v151
	ds_write_b128 v209, v[148:151] offset:1024
	v_mul_f32_e32 v152, v28, v152
	v_mul_f32_e32 v153, v28, v153
	v_mul_f32_e32 v154, v28, v154
	v_mul_f32_e32 v155, v28, v155
	ds_write_b128 v209, v[152:155] offset:2048
	v_mul_f32_e32 v156, v29, v156
	v_mul_f32_e32 v157, v29, v157
	v_mul_f32_e32 v158, v29, v158
	v_mul_f32_e32 v159, v29, v159
	ds_write_b128 v209, v[156:159] offset:3072
	v_mul_f32_e32 v160, v30, v160
	v_mul_f32_e32 v161, v30, v161
	v_mul_f32_e32 v162, v30, v162
	v_mul_f32_e32 v163, v30, v163
	ds_write_b128 v209, v[160:163] offset:4096
	v_mul_f32_e32 v164, v31, v164
	v_mul_f32_e32 v165, v31, v165
	v_mul_f32_e32 v166, v31, v166
	v_mul_f32_e32 v167, v31, v167
	ds_write_b128 v209, v[164:167] offset:5120
	v_mul_f32_e32 v168, v32, v168
	v_mul_f32_e32 v169, v32, v169
	v_mul_f32_e32 v170, v32, v170
	v_mul_f32_e32 v171, v32, v171
	ds_write_b128 v209, v[168:171] offset:6144
	v_mul_f32_e32 v172, v33, v172
	v_mul_f32_e32 v173, v33, v173
	v_mul_f32_e32 v174, v33, v174
	v_mul_f32_e32 v175, v33, v175
	ds_write_b128 v209, v[172:175] offset:7168
	s_waitcnt lgkmcnt(0)
	s_barrier
; #define GAS __attribute__((address_space(1)))
; #define LAS __attribute__((address_space(3)))
; #define LDS_WAIT() asm volatile("s_waitcnt lgkmcnt(0)" ::: "memory")
;     const int pr = item >> 1, kb = 2 * (pr / nblk) + (item & 1), nb = pr % nblk, k0 = 64 * kb, n0 = 32 * nb;
;     const int nr = n0 + (lane & 31); const int sc = MAP == 1 ? src_col_in(nr) : nr;
;     float v[32];
; #pragma unroll
;     for (int i = 0; i < 32; ++i) v[i] = sc >= 0 ? W[(size_t)(k0 + 2 * i + (lane >> 5)) * Nsrc + sc] : 0.f;
; #pragma unroll
;     for (int i = 0; i < 32; ++i) { const int k = k0 + 2 * i + (lane >> 5); float x = v[i] * wscale; if (KS) x *= (k < ksplit ? ksA[k] : ksB[k - ksplit]); scr[(2 * i + (lane >> 5)) * 33 + (lane & 31)] = x; }
;     LDS_WAIT(); asm volatile("" ::: "memory");
;     const int c = lane & 7;
; #pragma unroll
;     for (int j = 0; j < 4; ++j) { const int n = (lane >> 3) + 8 * j; const LAS float* s = scr + (8 * c) * 33 + n;
;         const unsigned long long o = (unsigned long long)pg8::pk4_fp8(s[0 * 33], s[1 * 33], s[2 * 33], s[3 * 33]) | ((unsigned long long)pg8::pk4_fp8(s[4 * 33], s[5 * 33], s[6 * 33], s[7 * 33]) << 32);
;         *(GAS unsigned long long*)(WT + (size_t)(n0 + n) * K + k0 + 8 * c) = o; }
;     LDS_WAIT(); asm volatile("" ::: "memory");
; __global__ void __launch_bounds__(NWAVES * 64, 2) hybrid_fwd(Args args) {
;     ...
;             if (r < I_UP) { p0_transpose_item_f8<true>(args.in[15] + (size_t)l * DM * FF, DM, FF, FF / 32, (unsigned char*)(ws + WS_WUP + l * SZ_WUP), WUP8_SCALE, args.in[14] + l * DM, args.in[14] + l * DM, DM, scr, r, lane); continue; } r -= I_UP;
	s_add_u32 s8, s30, 0x2000
	s_addc_u32 s9, s31, 0
	global_load_dwordx4 v[144:147], v74, s[8:9]
	s_add_u32 s8, s8, 0x20000
	s_addc_u32 s9, s9, 0
	global_load_dwordx4 v[148:151], v74, s[8:9]
	s_add_u32 s8, s8, 0x20000
	s_addc_u32 s9, s9, 0
	global_load_dwordx4 v[152:155], v74, s[8:9]
	s_add_u32 s8, s8, 0x20000
	s_addc_u32 s9, s9, 0
	global_load_dwordx4 v[156:159], v74, s[8:9]
	s_add_u32 s8, s8, 0x20000
	s_addc_u32 s9, s9, 0
	global_load_dwordx4 v[160:163], v74, s[8:9]
	s_add_u32 s8, s8, 0x20000
	s_addc_u32 s9, s9, 0
	global_load_dwordx4 v[164:167], v74, s[8:9]
	s_add_u32 s8, s8, 0x20000
	s_addc_u32 s9, s9, 0
	global_load_dwordx4 v[168:171], v74, s[8:9]
	s_add_u32 s8, s8, 0x20000
	s_addc_u32 s9, s9, 0
	global_load_dwordx4 v[172:175], v74, s[8:9]
	s_mov_b64 s[6:7], s[32:33]
	ds_read_b32 v226, v211
	ds_read_b32 v227, v211 offset:512
	ds_read_b32 v228, v211 offset:1024
	ds_read_b32 v229, v211 offset:1536
	ds_read_b32 v230, v211 offset:2048
	ds_read_b32 v231, v211 offset:2560
	ds_read_b32 v232, v211 offset:3072
	ds_read_b32 v233, v211 offset:3584
	ds_read_b32 v234, v211 offset:4096
	ds_read_b32 v235, v211 offset:4608
	ds_read_b32 v236, v211 offset:5120
	ds_read_b32 v237, v211 offset:5632
	ds_read_b32 v238, v211 offset:6144
	ds_read_b32 v239, v211 offset:6656
	ds_read_b32 v240, v211 offset:7168
	ds_read_b32 v241, v211 offset:7680
	s_waitcnt lgkmcnt(0)
	v_max_f32_e32 v226, v226, v226
	v_max_f32_e32 v227, v227, v227
	v_max_f32_e32 v228, v228, v228
	v_max_f32_e32 v229, v229, v229
	v_max_f32_e32 v230, v230, v230
	v_max_f32_e32 v231, v231, v231
	v_max_f32_e32 v232, v232, v232
	v_max_f32_e32 v233, v233, v233
	v_max_f32_e32 v234, v234, v234
	v_max_f32_e32 v235, v235, v235
	v_max_f32_e32 v236, v236, v236
	v_max_f32_e32 v237, v237, v237
	v_max_f32_e32 v238, v238, v238
	v_max_f32_e32 v239, v239, v239
	v_max_f32_e32 v240, v240, v240
	v_max_f32_e32 v241, v241, v241
	v_med3_f32 v226, v226, s62, v95
	v_med3_f32 v227, v227, s62, v95
	v_med3_f32 v228, v228, s62, v95
	v_med3_f32 v229, v229, s62, v95
	v_med3_f32 v230, v230, s62, v95
	v_med3_f32 v231, v231, s62, v95
	v_med3_f32 v232, v232, s62, v95
	v_med3_f32 v233, v233, s62, v95
	v_med3_f32 v234, v234, s62, v95
	v_med3_f32 v235, v235, s62, v95
	v_med3_f32 v236, v236, s62, v95
	v_med3_f32 v237, v237, s62, v95
	v_med3_f32 v238, v238, s62, v95
	v_med3_f32 v239, v239, s62, v95
	v_med3_f32 v240, v240, s62, v95
	v_med3_f32 v241, v241, s62, v95
	v_mov_b32_e32 v242, 0
	v_mov_b32_e32 v243, 0
	v_mov_b32_e32 v244, 0
	v_mov_b32_e32 v245, 0
	v_cvt_pk_fp8_f32 v242, v226, v227
	v_cvt_pk_fp8_f32 v243, v230, v231
	v_cvt_pk_fp8_f32 v244, v234, v235
	v_cvt_pk_fp8_f32 v245, v238, v239
	v_cvt_pk_fp8_f32 v242, v228, v229 op_sel:[0,0,1]
	v_cvt_pk_fp8_f32 v243, v232, v233 op_sel:[0,0,1]
	v_cvt_pk_fp8_f32 v244, v236, v237 op_sel:[0,0,1]
	v_cvt_pk_fp8_f32 v245, v240, v241 op_sel:[0,0,1]
	s_nop 0
	global_store_dwordx4 v77, v[242:245], s[6:7]
	ds_read_b32 v226, v213
	ds_read_b32 v227, v213 offset:512
	ds_read_b32 v228, v213 offset:1024
	ds_read_b32 v229, v213 offset:1536
	ds_read_b32 v230, v213 offset:2048
	ds_read_b32 v231, v213 offset:2560
	ds_read_b32 v232, v213 offset:3072
	ds_read_b32 v233, v213 offset:3584
	ds_read_b32 v234, v213 offset:4096
	ds_read_b32 v235, v213 offset:4608
	ds_read_b32 v236, v213 offset:5120
	ds_read_b32 v237, v213 offset:5632
	ds_read_b32 v238, v213 offset:6144
	ds_read_b32 v239, v213 offset:6656
	ds_read_b32 v240, v213 offset:7168
	ds_read_b32 v241, v213 offset:7680
	s_waitcnt lgkmcnt(0)
	v_max_f32_e32 v226, v226, v226
	v_max_f32_e32 v227, v227, v227
	v_max_f32_e32 v228, v228, v228
	v_max_f32_e32 v229, v229, v229
	v_max_f32_e32 v230, v230, v230
	v_max_f32_e32 v231, v231, v231
	v_max_f32_e32 v232, v232, v232
	v_max_f32_e32 v233, v233, v233
	v_max_f32_e32 v234, v234, v234
	v_max_f32_e32 v235, v235, v235
	v_max_f32_e32 v236, v236, v236
	v_max_f32_e32 v237, v237, v237
	v_max_f32_e32 v238, v238, v238
	v_max_f32_e32 v239, v239, v239
	v_max_f32_e32 v240, v240, v240
	v_max_f32_e32 v241, v241, v241
	v_med3_f32 v226, v226, s62, v95
	v_med3_f32 v227, v227, s62, v95
	v_med3_f32 v228, v228, s62, v95
	v_med3_f32 v229, v229, s62, v95
	v_med3_f32 v230, v230, s62, v95
	v_med3_f32 v231, v231, s62, v95
	v_med3_f32 v232, v232, s62, v95
	v_med3_f32 v233, v233, s62, v95
	v_med3_f32 v234, v234, s62, v95
	v_med3_f32 v235, v235, s62, v95
	v_med3_f32 v236, v236, s62, v95
	v_med3_f32 v237, v237, s62, v95
	v_med3_f32 v238, v238, s62, v95
	v_med3_f32 v239, v239, s62, v95
	v_med3_f32 v240, v240, s62, v95
	v_med3_f32 v241, v241, s62, v95
	v_mov_b32_e32 v242, 0
	v_mov_b32_e32 v243, 0
	v_mov_b32_e32 v244, 0
	v_mov_b32_e32 v245, 0
	v_cvt_pk_fp8_f32 v242, v226, v227
	v_cvt_pk_fp8_f32 v243, v230, v231
	v_cvt_pk_fp8_f32 v244, v234, v235
	v_cvt_pk_fp8_f32 v245, v238, v239
	v_cvt_pk_fp8_f32 v242, v228, v229 op_sel:[0,0,1]
	v_cvt_pk_fp8_f32 v243, v232, v233 op_sel:[0,0,1]
	v_cvt_pk_fp8_f32 v244, v236, v237 op_sel:[0,0,1]
	v_cvt_pk_fp8_f32 v245, v240, v241 op_sel:[0,0,1]
	s_nop 0
	global_store_dwordx4 v78, v[242:245], s[6:7]
	s_waitcnt vmcnt(10)
	v_mul_f32_e32 v176, v26, v176
	v_mul_f32_e32 v177, v26, v177
	v_mul_f32_e32 v178, v26, v178
	v_mul_f32_e32 v179, v26, v179
	ds_write_b128 v210, v[176:179]
	v_mul_f32_e32 v180, v27, v180
	v_mul_f32_e32 v181, v27, v181
	v_mul_f32_e32 v182, v27, v182
	v_mul_f32_e32 v183, v27, v183
	ds_write_b128 v210, v[180:183] offset:1024
	v_mul_f32_e32 v184, v28, v184
	v_mul_f32_e32 v185, v28, v185
	v_mul_f32_e32 v186, v28, v186
	v_mul_f32_e32 v187, v28, v187
	ds_write_b128 v210, v[184:187] offset:2048
	v_mul_f32_e32 v188, v29, v188
	v_mul_f32_e32 v189, v29, v189
	v_mul_f32_e32 v190, v29, v190
	v_mul_f32_e32 v191, v29, v191
	ds_write_b128 v210, v[188:191] offset:3072
	v_mul_f32_e32 v192, v30, v192
	v_mul_f32_e32 v193, v30, v193
	v_mul_f32_e32 v194, v30, v194
	v_mul_f32_e32 v195, v30, v195
	ds_write_b128 v210, v[192:195] offset:4096
	v_mul_f32_e32 v196, v31, v196
	v_mul_f32_e32 v197, v31, v197
	v_mul_f32_e32 v198, v31, v198
	v_mul_f32_e32 v199, v31, v199
	ds_write_b128 v210, v[196:199] offset:5120
	v_mul_f32_e32 v200, v32, v200
	v_mul_f32_e32 v201, v32, v201
	v_mul_f32_e32 v202, v32, v202
	v_mul_f32_e32 v203, v32, v203
	ds_write_b128 v210, v[200:203] offset:6144
	v_mul_f32_e32 v204, v33, v204
	v_mul_f32_e32 v205, v33, v205
	v_mul_f32_e32 v206, v33, v206
	v_mul_f32_e32 v207, v33, v207
	ds_write_b128 v210, v[204:207] offset:7168
	s_waitcnt lgkmcnt(0)
	s_barrier
; #define GAS __attribute__((address_space(1)))
; #define LAS __attribute__((address_space(3)))
; #define LDS_WAIT() asm volatile("s_waitcnt lgkmcnt(0)" ::: "memory")
;     const int pr = item >> 1, kb = 2 * (pr / nblk) + (item & 1), nb = pr % nblk, k0 = 64 * kb, n0 = 32 * nb;
;     const int nr = n0 + (lane & 31); const int sc = MAP == 1 ? src_col_in(nr) : nr;
;     float v[32];
; #pragma unroll
;     for (int i = 0; i < 32; ++i) v[i] = sc >= 0 ? W[(size_t)(k0 + 2 * i + (lane >> 5)) * Nsrc + sc] : 0.f;
; #pragma unroll
;     for (int i = 0; i < 32; ++i) { const int k = k0 + 2 * i + (lane >> 5); float x = v[i] * wscale; if (KS) x *= (k < ksplit ? ksA[k] : ksB[k - ksplit]); scr[(2 * i + (lane >> 5)) * 33 + (lane & 31)] = x; }
;     LDS_WAIT(); asm volatile("" ::: "memory");
;     const int c = lane & 7;
; #pragma unroll
;     for (int j = 0; j < 4; ++j) { const int n = (lane >> 3) + 8 * j; const LAS float* s = scr + (8 * c) * 33 + n;
;         const unsigned long long o = (unsigned long long)pg8::pk4_fp8(s[0 * 33], s[1 * 33], s[2 * 33], s[3 * 33]) | ((unsigned long long)pg8::pk4_fp8(s[4 * 33], s[5 * 33], s[6 * 33], s[7 * 33]) << 32);
;         *(GAS unsigned long long*)(WT + (size_t)(n0 + n) * K + k0 + 8 * c) = o; }
;     LDS_WAIT(); asm volatile("" ::: "memory");
; __global__ void __launch_bounds__(NWAVES * 64, 2) hybrid_fwd(Args args) {
;     ...
;             if (r < I_UP) { p0_transpose_item_f8<true>(args.in[15] + (size_t)l * DM * FF, DM, FF, FF / 32, (unsigned char*)(ws + WS_WUP + l * SZ_WUP), WUP8_SCALE, args.in[14] + l * DM, args.in[14] + l * DM, DM, scr, r, lane); continue; } r -= I_UP;
	s_add_u32 s8, s30, 0x3000
	s_addc_u32 s9, s31, 0
	global_load_dwordx4 v[176:179], v74, s[8:9]
	s_add_u32 s8, s8, 0x20000
	s_addc_u32 s9, s9, 0
	global_load_dwordx4 v[180:183], v74, s[8:9]
	s_add_u32 s8, s8, 0x20000
	s_addc_u32 s9, s9, 0
	global_load_dwordx4 v[184:187], v74, s[8:9]
	s_add_u32 s8, s8, 0x20000
	s_addc_u32 s9, s9, 0
	global_load_dwordx4 v[188:191], v74, s[8:9]
	s_add_u32 s8, s8, 0x20000
	s_addc_u32 s9, s9, 0
	global_load_dwordx4 v[192:195], v74, s[8:9]
	s_add_u32 s8, s8, 0x20000
	s_addc_u32 s9, s9, 0
	global_load_dwordx4 v[196:199], v74, s[8:9]
	s_add_u32 s8, s8, 0x20000
	s_addc_u32 s9, s9, 0
	global_load_dwordx4 v[200:203], v74, s[8:9]
	s_add_u32 s8, s8, 0x20000
	s_addc_u32 s9, s9, 0
	global_load_dwordx4 v[204:207], v74, s[8:9]
	s_add_u32 s6, s32, 0x400000
	s_addc_u32 s7, s33, 0
	ds_read_b32 v226, v212
	ds_read_b32 v227, v212 offset:512
	ds_read_b32 v228, v212 offset:1024
	ds_read_b32 v229, v212 offset:1536
	ds_read_b32 v230, v212 offset:2048
	ds_read_b32 v231, v212 offset:2560
	ds_read_b32 v232, v212 offset:3072
	ds_read_b32 v233, v212 offset:3584
	ds_read_b32 v234, v212 offset:4096
	ds_read_b32 v235, v212 offset:4608
	ds_read_b32 v236, v212 offset:5120
	ds_read_b32 v237, v212 offset:5632
	ds_read_b32 v238, v212 offset:6144
	ds_read_b32 v239, v212 offset:6656
	ds_read_b32 v240, v212 offset:7168
	ds_read_b32 v241, v212 offset:7680
	s_waitcnt lgkmcnt(0)
	v_max_f32_e32 v226, v226, v226
	v_max_f32_e32 v227, v227, v227
	v_max_f32_e32 v228, v228, v228
	v_max_f32_e32 v229, v229, v229
	v_max_f32_e32 v230, v230, v230
	v_max_f32_e32 v231, v231, v231
	v_max_f32_e32 v232, v232, v232
	v_max_f32_e32 v233, v233, v233
	v_max_f32_e32 v234, v234, v234
	v_max_f32_e32 v235, v235, v235
	v_max_f32_e32 v236, v236, v236
	v_max_f32_e32 v237, v237, v237
	v_max_f32_e32 v238, v238, v238
	v_max_f32_e32 v239, v239, v239
	v_max_f32_e32 v240, v240, v240
	v_max_f32_e32 v241, v241, v241
	v_med3_f32 v226, v226, s62, v95
	v_med3_f32 v227, v227, s62, v95
	v_med3_f32 v228, v228, s62, v95
	v_med3_f32 v229, v229, s62, v95
	v_med3_f32 v230, v230, s62, v95
	v_med3_f32 v231, v231, s62, v95
	v_med3_f32 v232, v232, s62, v95
	v_med3_f32 v233, v233, s62, v95
	v_med3_f32 v234, v234, s62, v95
	v_med3_f32 v235, v235, s62, v95
	v_med3_f32 v236, v236, s62, v95
	v_med3_f32 v237, v237, s62, v95
	v_med3_f32 v238, v238, s62, v95
	v_med3_f32 v239, v239, s62, v95
	v_med3_f32 v240, v240, s62, v95
	v_med3_f32 v241, v241, s62, v95
	v_mov_b32_e32 v242, 0
	v_mov_b32_e32 v243, 0
	v_mov_b32_e32 v244, 0
	v_mov_b32_e32 v245, 0
	v_cvt_pk_fp8_f32 v242, v226, v227
	v_cvt_pk_fp8_f32 v243, v230, v231
	v_cvt_pk_fp8_f32 v244, v234, v235
	v_cvt_pk_fp8_f32 v245, v238, v239
	v_cvt_pk_fp8_f32 v242, v228, v229 op_sel:[0,0,1]
	v_cvt_pk_fp8_f32 v243, v232, v233 op_sel:[0,0,1]
	v_cvt_pk_fp8_f32 v244, v236, v237 op_sel:[0,0,1]
	v_cvt_pk_fp8_f32 v245, v240, v241 op_sel:[0,0,1]
	s_nop 0
	global_store_dwordx4 v77, v[242:245], s[6:7]
	ds_read_b32 v226, v214
	ds_read_b32 v227, v214 offset:512
	ds_read_b32 v228, v214 offset:1024
	ds_read_b32 v229, v214 offset:1536
	ds_read_b32 v230, v214 offset:2048
	ds_read_b32 v231, v214 offset:2560
	ds_read_b32 v232, v214 offset:3072
	ds_read_b32 v233, v214 offset:3584
	ds_read_b32 v234, v214 offset:4096
	ds_read_b32 v235, v214 offset:4608
	ds_read_b32 v236, v214 offset:5120
	ds_read_b32 v237, v214 offset:5632
	ds_read_b32 v238, v214 offset:6144
	ds_read_b32 v239, v214 offset:6656
	ds_read_b32 v240, v214 offset:7168
	ds_read_b32 v241, v214 offset:7680
	s_waitcnt lgkmcnt(0)
	v_max_f32_e32 v226, v226, v226
	v_max_f32_e32 v227, v227, v227
	v_max_f32_e32 v228, v228, v228
	v_max_f32_e32 v229, v229, v229
	v_max_f32_e32 v230, v230, v230
	v_max_f32_e32 v231, v231, v231
	v_max_f32_e32 v232, v232, v232
	v_max_f32_e32 v233, v233, v233
	v_max_f32_e32 v234, v234, v234
	v_max_f32_e32 v235, v235, v235
	v_max_f32_e32 v236, v236, v236
	v_max_f32_e32 v237, v237, v237
	v_max_f32_e32 v238, v238, v238
	v_max_f32_e32 v239, v239, v239
	v_max_f32_e32 v240, v240, v240
	v_max_f32_e32 v241, v241, v241
	v_med3_f32 v226, v226, s62, v95
	v_med3_f32 v227, v227, s62, v95
	v_med3_f32 v228, v228, s62, v95
	v_med3_f32 v229, v229, s62, v95
	v_med3_f32 v230, v230, s62, v95
	v_med3_f32 v231, v231, s62, v95
	v_med3_f32 v232, v232, s62, v95
	v_med3_f32 v233, v233, s62, v95
	v_med3_f32 v234, v234, s62, v95
	v_med3_f32 v235, v235, s62, v95
	v_med3_f32 v236, v236, s62, v95
	v_med3_f32 v237, v237, s62, v95
	v_med3_f32 v238, v238, s62, v95
	v_med3_f32 v239, v239, s62, v95
	v_med3_f32 v240, v240, s62, v95
	v_med3_f32 v241, v241, s62, v95
	v_mov_b32_e32 v242, 0
	v_mov_b32_e32 v243, 0
	v_mov_b32_e32 v244, 0
	v_mov_b32_e32 v245, 0
	v_cvt_pk_fp8_f32 v242, v226, v227
	v_cvt_pk_fp8_f32 v243, v230, v231
	v_cvt_pk_fp8_f32 v244, v234, v235
	v_cvt_pk_fp8_f32 v245, v238, v239
	v_cvt_pk_fp8_f32 v242, v228, v229 op_sel:[0,0,1]
	v_cvt_pk_fp8_f32 v243, v232, v233 op_sel:[0,0,1]
	v_cvt_pk_fp8_f32 v244, v236, v237 op_sel:[0,0,1]
	v_cvt_pk_fp8_f32 v245, v240, v241 op_sel:[0,0,1]
	s_nop 0
	global_store_dwordx4 v78, v[242:245], s[6:7]
	s_waitcnt vmcnt(12)
	v_mul_f32_e32 v144, v26, v144
	v_mul_f32_e32 v145, v26, v145
	v_mul_f32_e32 v146, v26, v146
	v_mul_f32_e32 v147, v26, v147
	ds_write_b128 v209, v[144:147]
	v_mul_f32_e32 v148, v27, v148
	v_mul_f32_e32 v149, v27, v149
	v_mul_f32_e32 v150, v27, v150
	v_mul_f32_e32 v151, v27, v151
	ds_write_b128 v209, v[148:151] offset:1024
	v_mul_f32_e32 v152, v28, v152
	v_mul_f32_e32 v153, v28, v153
	v_mul_f32_e32 v154, v28, v154
	v_mul_f32_e32 v155, v28, v155
	ds_write_b128 v209, v[152:155] offset:2048
	v_mul_f32_e32 v156, v29, v156
	v_mul_f32_e32 v157, v29, v157
	v_mul_f32_e32 v158, v29, v158
	v_mul_f32_e32 v159, v29, v159
	ds_write_b128 v209, v[156:159] offset:3072
	v_mul_f32_e32 v160, v30, v160
	v_mul_f32_e32 v161, v30, v161
	v_mul_f32_e32 v162, v30, v162
	v_mul_f32_e32 v163, v30, v163
	ds_write_b128 v209, v[160:163] offset:4096
	v_mul_f32_e32 v164, v31, v164
	v_mul_f32_e32 v165, v31, v165
	v_mul_f32_e32 v166, v31, v166
	v_mul_f32_e32 v167, v31, v167
	ds_write_b128 v209, v[164:167] offset:5120
	v_mul_f32_e32 v168, v32, v168
	v_mul_f32_e32 v169, v32, v169
	v_mul_f32_e32 v170, v32, v170
	v_mul_f32_e32 v171, v32, v171
	ds_write_b128 v209, v[168:171] offset:6144
	v_mul_f32_e32 v172, v33, v172
	v_mul_f32_e32 v173, v33, v173
	v_mul_f32_e32 v174, v33, v174
	v_mul_f32_e32 v175, v33, v175
	ds_write_b128 v209, v[172:175] offset:7168
	s_waitcnt lgkmcnt(0)
	s_barrier
; #define GAS __attribute__((address_space(1)))
; #define LAS __attribute__((address_space(3)))
; #define LDS_WAIT() asm volatile("s_waitcnt lgkmcnt(0)" ::: "memory")
;     const int pr = item >> 1, kb = 2 * (pr / nblk) + (item & 1), nb = pr % nblk, k0 = 64 * kb, n0 = 32 * nb;
;     const int nr = n0 + (lane & 31); const int sc = MAP == 1 ? src_col_in(nr) : nr;
;     float v[32];
; #pragma unroll
;     for (int i = 0; i < 32; ++i) v[i] = sc >= 0 ? W[(size_t)(k0 + 2 * i + (lane >> 5)) * Nsrc + sc] : 0.f;
; #pragma unroll
;     for (int i = 0; i < 32; ++i) { const int k = k0 + 2 * i + (lane >> 5); float x = v[i] * wscale; if (KS) x *= (k < ksplit ? ksA[k] : ksB[k - ksplit]); scr[(2 * i + (lane >> 5)) * 33 + (lane & 31)] = x; }
;     LDS_WAIT(); asm volatile("" ::: "memory");
;     const int c = lane & 7;
; #pragma unroll
;     for (int j = 0; j < 4; ++j) { const int n = (lane >> 3) + 8 * j; const LAS float* s = scr + (8 * c) * 33 + n;
;         const unsigned long long o = (unsigned long long)pg8::pk4_fp8(s[0 * 33], s[1 * 33], s[2 * 33], s[3 * 33]) | ((unsigned long long)pg8::pk4_fp8(s[4 * 33], s[5 * 33], s[6 * 33], s[7 * 33]) << 32);
;         *(GAS unsigned long long*)(WT + (size_t)(n0 + n) * K + k0 + 8 * c) = o; }
;     LDS_WAIT(); asm volatile("" ::: "memory");
; __global__ void __launch_bounds__(NWAVES * 64, 2) hybrid_fwd(Args args) {
;     ...
;             if (r < I_UP) { p0_transpose_item_f8<true>(args.in[15] + (size_t)l * DM * FF, DM, FF, FF / 32, (unsigned char*)(ws + WS_WUP + l * SZ_WUP), WUP8_SCALE, args.in[14] + l * DM, args.in[14] + l * DM, DM, scr, r, lane); continue; } r -= I_UP;
	s_add_u32 s8, s30, 0x4000
	s_addc_u32 s9, s31, 0
	global_load_dwordx4 v[144:147], v74, s[8:9]
	s_add_u32 s8, s8, 0x20000
	s_addc_u32 s9, s9, 0
	global_load_dwordx4 v[148:151], v74, s[8:9]
	s_add_u32 s8, s8, 0x20000
	s_addc_u32 s9, s9, 0
	global_load_dwordx4 v[152:155], v74, s[8:9]
	s_add_u32 s8, s8, 0x20000
	s_addc_u32 s9, s9, 0
	global_load_dwordx4 v[156:159], v74, s[8:9]
	s_add_u32 s8, s8, 0x20000
	s_addc_u32 s9, s9, 0
	global_load_dwordx4 v[160:163], v74, s[8:9]
	s_add_u32 s8, s8, 0x20000
	s_addc_u32 s9, s9, 0
	global_load_dwordx4 v[164:167], v74, s[8:9]
	s_add_u32 s8, s8, 0x20000
	s_addc_u32 s9, s9, 0
	global_load_dwordx4 v[168:171], v74, s[8:9]
	s_add_u32 s8, s8, 0x20000
	s_addc_u32 s9, s9, 0
	global_load_dwordx4 v[172:175], v74, s[8:9]
	s_add_u32 s6, s32, 0x800000
	s_addc_u32 s7, s33, 0
	ds_read_b32 v226, v211
	ds_read_b32 v227, v211 offset:512
	ds_read_b32 v228, v211 offset:1024
	ds_read_b32 v229, v211 offset:1536
	ds_read_b32 v230, v211 offset:2048
	ds_read_b32 v231, v211 offset:2560
	ds_read_b32 v232, v211 offset:3072
	ds_read_b32 v233, v211 offset:3584
	ds_read_b32 v234, v211 offset:4096
	ds_read_b32 v235, v211 offset:4608
	ds_read_b32 v236, v211 offset:5120
	ds_read_b32 v237, v211 offset:5632
	ds_read_b32 v238, v211 offset:6144
	ds_read_b32 v239, v211 offset:6656
	ds_read_b32 v240, v211 offset:7168
	ds_read_b32 v241, v211 offset:7680
	s_waitcnt lgkmcnt(0)
	v_max_f32_e32 v226, v226, v226
	v_max_f32_e32 v227, v227, v227
	v_max_f32_e32 v228, v228, v228
	v_max_f32_e32 v229, v229, v229
	v_max_f32_e32 v230, v230, v230
	v_max_f32_e32 v231, v231, v231
	v_max_f32_e32 v232, v232, v232
	v_max_f32_e32 v233, v233, v233
	v_max_f32_e32 v234, v234, v234
	v_max_f32_e32 v235, v235, v235
	v_max_f32_e32 v236, v236, v236
	v_max_f32_e32 v237, v237, v237
	v_max_f32_e32 v238, v238, v238
	v_max_f32_e32 v239, v239, v239
	v_max_f32_e32 v240, v240, v240
	v_max_f32_e32 v241, v241, v241
	v_med3_f32 v226, v226, s62, v95
	v_med3_f32 v227, v227, s62, v95
	v_med3_f32 v228, v228, s62, v95
	v_med3_f32 v229, v229, s62, v95
	v_med3_f32 v230, v230, s62, v95
	v_med3_f32 v231, v231, s62, v95
	v_med3_f32 v232, v232, s62, v95
	v_med3_f32 v233, v233, s62, v95
	v_med3_f32 v234, v234, s62, v95
	v_med3_f32 v235, v235, s62, v95
	v_med3_f32 v236, v236, s62, v95
	v_med3_f32 v237, v237, s62, v95
	v_med3_f32 v238, v238, s62, v95
	v_med3_f32 v239, v239, s62, v95
	v_med3_f32 v240, v240, s62, v95
	v_med3_f32 v241, v241, s62, v95
	v_mov_b32_e32 v242, 0
	v_mov_b32_e32 v243, 0
	v_mov_b32_e32 v244, 0
	v_mov_b32_e32 v245, 0
	v_cvt_pk_fp8_f32 v242, v226, v227
	v_cvt_pk_fp8_f32 v243, v230, v231
	v_cvt_pk_fp8_f32 v244, v234, v235
	v_cvt_pk_fp8_f32 v245, v238, v239
	v_cvt_pk_fp8_f32 v242, v228, v229 op_sel:[0,0,1]
	v_cvt_pk_fp8_f32 v243, v232, v233 op_sel:[0,0,1]
	v_cvt_pk_fp8_f32 v244, v236, v237 op_sel:[0,0,1]
	v_cvt_pk_fp8_f32 v245, v240, v241 op_sel:[0,0,1]
	s_nop 0
	global_store_dwordx4 v77, v[242:245], s[6:7]
	ds_read_b32 v226, v213
	ds_read_b32 v227, v213 offset:512
	ds_read_b32 v228, v213 offset:1024
	ds_read_b32 v229, v213 offset:1536
	ds_read_b32 v230, v213 offset:2048
	ds_read_b32 v231, v213 offset:2560
	ds_read_b32 v232, v213 offset:3072
	ds_read_b32 v233, v213 offset:3584
	ds_read_b32 v234, v213 offset:4096
	ds_read_b32 v235, v213 offset:4608
	ds_read_b32 v236, v213 offset:5120
	ds_read_b32 v237, v213 offset:5632
	ds_read_b32 v238, v213 offset:6144
	ds_read_b32 v239, v213 offset:6656
	ds_read_b32 v240, v213 offset:7168
	ds_read_b32 v241, v213 offset:7680
	s_waitcnt lgkmcnt(0)
	v_max_f32_e32 v226, v226, v226
	v_max_f32_e32 v227, v227, v227
	v_max_f32_e32 v228, v228, v228
	v_max_f32_e32 v229, v229, v229
	v_max_f32_e32 v230, v230, v230
	v_max_f32_e32 v231, v231, v231
	v_max_f32_e32 v232, v232, v232
	v_max_f32_e32 v233, v233, v233
	v_max_f32_e32 v234, v234, v234
	v_max_f32_e32 v235, v235, v235
	v_max_f32_e32 v236, v236, v236
	v_max_f32_e32 v237, v237, v237
	v_max_f32_e32 v238, v238, v238
	v_max_f32_e32 v239, v239, v239
	v_max_f32_e32 v240, v240, v240
	v_max_f32_e32 v241, v241, v241
	v_med3_f32 v226, v226, s62, v95
	v_med3_f32 v227, v227, s62, v95
	v_med3_f32 v228, v228, s62, v95
	v_med3_f32 v229, v229, s62, v95
	v_med3_f32 v230, v230, s62, v95
	v_med3_f32 v231, v231, s62, v95
	v_med3_f32 v232, v232, s62, v95
	v_med3_f32 v233, v233, s62, v95
	v_med3_f32 v234, v234, s62, v95
	v_med3_f32 v235, v235, s62, v95
	v_med3_f32 v236, v236, s62, v95
	v_med3_f32 v237, v237, s62, v95
	v_med3_f32 v238, v238, s62, v95
	v_med3_f32 v239, v239, s62, v95
	v_med3_f32 v240, v240, s62, v95
	v_med3_f32 v241, v241, s62, v95
	v_mov_b32_e32 v242, 0
	v_mov_b32_e32 v243, 0
	v_mov_b32_e32 v244, 0
	v_mov_b32_e32 v245, 0
	v_cvt_pk_fp8_f32 v242, v226, v227
	v_cvt_pk_fp8_f32 v243, v230, v231
	v_cvt_pk_fp8_f32 v244, v234, v235
	v_cvt_pk_fp8_f32 v245, v238, v239
	v_cvt_pk_fp8_f32 v242, v228, v229 op_sel:[0,0,1]
	v_cvt_pk_fp8_f32 v243, v232, v233 op_sel:[0,0,1]
	v_cvt_pk_fp8_f32 v244, v236, v237 op_sel:[0,0,1]
	v_cvt_pk_fp8_f32 v245, v240, v241 op_sel:[0,0,1]
	s_nop 0
	global_store_dwordx4 v78, v[242:245], s[6:7]
	s_waitcnt vmcnt(12)
	v_mul_f32_e32 v176, v26, v176
	v_mul_f32_e32 v177, v26, v177
	v_mul_f32_e32 v178, v26, v178
	v_mul_f32_e32 v179, v26, v179
	ds_write_b128 v210, v[176:179]
	v_mul_f32_e32 v180, v27, v180
	v_mul_f32_e32 v181, v27, v181
	v_mul_f32_e32 v182, v27, v182
	v_mul_f32_e32 v183, v27, v183
	ds_write_b128 v210, v[180:183] offset:1024
	v_mul_f32_e32 v184, v28, v184
	v_mul_f32_e32 v185, v28, v185
	v_mul_f32_e32 v186, v28, v186
	v_mul_f32_e32 v187, v28, v187
	ds_write_b128 v210, v[184:187] offset:2048
	v_mul_f32_e32 v188, v29, v188
	v_mul_f32_e32 v189, v29, v189
	v_mul_f32_e32 v190, v29, v190
	v_mul_f32_e32 v191, v29, v191
	ds_write_b128 v210, v[188:191] offset:3072
	v_mul_f32_e32 v192, v30, v192
	v_mul_f32_e32 v193, v30, v193
	v_mul_f32_e32 v194, v30, v194
	v_mul_f32_e32 v195, v30, v195
	ds_write_b128 v210, v[192:195] offset:4096
	v_mul_f32_e32 v196, v31, v196
	v_mul_f32_e32 v197, v31, v197
	v_mul_f32_e32 v198, v31, v198
	v_mul_f32_e32 v199, v31, v199
	ds_write_b128 v210, v[196:199] offset:5120
	v_mul_f32_e32 v200, v32, v200
	v_mul_f32_e32 v201, v32, v201
	v_mul_f32_e32 v202, v32, v202
	v_mul_f32_e32 v203, v32, v203
	ds_write_b128 v210, v[200:203] offset:6144
	v_mul_f32_e32 v204, v33, v204
	v_mul_f32_e32 v205, v33, v205
	v_mul_f32_e32 v206, v33, v206
	v_mul_f32_e32 v207, v33, v207
	ds_write_b128 v210, v[204:207] offset:7168
	s_waitcnt lgkmcnt(0)
	s_barrier
; #define GAS __attribute__((address_space(1)))
; #define LAS __attribute__((address_space(3)))
; #define LDS_WAIT() asm volatile("s_waitcnt lgkmcnt(0)" ::: "memory")
; __device__ __forceinline__ unsigned pk4_fp8(float a, float b, float c, float d) {
;     a = fminf(fmaxf(a, -448.f), 448.f); b = fminf(fmaxf(b, -448.f), 448.f); c = fminf(fmaxf(c, -448.f), 448.f); d = fminf(fmaxf(d, -448.f), 448.f);
;     int w = __builtin_amdgcn_cvt_pk_fp8_f32(a, b, 0, false); w = __builtin_amdgcn_cvt_pk_fp8_f32(c, d, w, true); return (unsigned)w; }
;     const int pr = item >> 1, kb = 2 * (pr / nblk) + (item & 1), nb = pr % nblk, k0 = 64 * kb, n0 = 32 * nb;
;     const int nr = n0 + (lane & 31); const int sc = MAP == 1 ? src_col_in(nr) : nr;
;     float v[32];
; #pragma unroll
;     for (int i = 0; i < 32; ++i) v[i] = sc >= 0 ? W[(size_t)(k0 + 2 * i + (lane >> 5)) * Nsrc + sc] : 0.f;
; #pragma unroll
;     for (int i = 0; i < 32; ++i) { const int k = k0 + 2 * i + (lane >> 5); float x = v[i] * wscale; if (KS) x *= (k < ksplit ? ksA[k] : ksB[k - ksplit]); scr[(2 * i + (lane >> 5)) * 33 + (lane & 31)] = x; }
;     LDS_WAIT(); asm volatile("" ::: "memory");
;     const int c = lane & 7;
; #pragma unroll
;     for (int j = 0; j < 4; ++j) { const int n = (lane >> 3) + 8 * j; const LAS float* s = scr + (8 * c) * 33 + n;
;         const unsigned long long o = (unsigned long long)pg8::pk4_fp8(s[0 * 33], s[1 * 33], s[2 * 33], s[3 * 33]) | ((unsigned long long)pg8::pk4_fp8(s[4 * 33], s[5 * 33], s[6 * 33], s[7 * 33]) << 32);
;         *(GAS unsigned long long*)(WT + (size_t)(n0 + n) * K + k0 + 8 * c) = o; }
;     LDS_WAIT(); asm volatile("" ::: "memory");
	s_add_u32 s8, s30, 0x5000
	s_addc_u32 s9, s31, 0
	global_load_dwordx4 v[176:179], v74, s[8:9]
	s_add_u32 s8, s8, 0x20000
	s_addc_u32 s9, s9, 0
	global_load_dwordx4 v[180:183], v74, s[8:9]
	s_add_u32 s8, s8, 0x20000
	s_addc_u32 s9, s9, 0
	global_load_dwordx4 v[184:187], v74, s[8:9]
	s_add_u32 s8, s8, 0x20000
	s_addc_u32 s9, s9, 0
	global_load_dwordx4 v[188:191], v74, s[8:9]
	s_add_u32 s8, s8, 0x20000
	s_addc_u32 s9, s9, 0
	global_load_dwordx4 v[192:195], v74, s[8:9]
	s_add_u32 s8, s8, 0x20000
	s_addc_u32 s9, s9, 0
	global_load_dwordx4 v[196:199], v74, s[8:9]
	s_add_u32 s8, s8, 0x20000
	s_addc_u32 s9, s9, 0
	global_load_dwordx4 v[200:203], v74, s[8:9]
	s_add_u32 s8, s8, 0x20000
	s_addc_u32 s9, s9, 0
	global_load_dwordx4 v[204:207], v74, s[8:9]
	s_add_u32 s6, s32, 0xc00000
	s_addc_u32 s7, s33, 0
	ds_read_b32 v226, v212
	ds_read_b32 v227, v212 offset:512
	ds_read_b32 v228, v212 offset:1024
	ds_read_b32 v229, v212 offset:1536
	ds_read_b32 v230, v212 offset:2048
	ds_read_b32 v231, v212 offset:2560
	ds_read_b32 v232, v212 offset:3072
	ds_read_b32 v233, v212 offset:3584
	ds_read_b32 v234, v212 offset:4096
	ds_read_b32 v235, v212 offset:4608
	ds_read_b32 v236, v212 offset:5120
	ds_read_b32 v237, v212 offset:5632
	ds_read_b32 v238, v212 offset:6144
	ds_read_b32 v239, v212 offset:6656
	ds_read_b32 v240, v212 offset:7168
	ds_read_b32 v241, v212 offset:7680
	s_waitcnt lgkmcnt(0)
	v_max_f32_e32 v226, v226, v226
	v_max_f32_e32 v227, v227, v227
	v_max_f32_e32 v228, v228, v228
	v_max_f32_e32 v229, v229, v229
	v_max_f32_e32 v230, v230, v230
	v_max_f32_e32 v231, v231, v231
	v_max_f32_e32 v232, v232, v232
	v_max_f32_e32 v233, v233, v233
	v_max_f32_e32 v234, v234, v234
	v_max_f32_e32 v235, v235, v235
	v_max_f32_e32 v236, v236, v236
	v_max_f32_e32 v237, v237, v237
	v_max_f32_e32 v238, v238, v238
	v_max_f32_e32 v239, v239, v239
	v_max_f32_e32 v240, v240, v240
	v_max_f32_e32 v241, v241, v241
	v_med3_f32 v226, v226, s62, v95
	v_med3_f32 v227, v227, s62, v95
	v_med3_f32 v228, v228, s62, v95
	v_med3_f32 v229, v229, s62, v95
	v_med3_f32 v230, v230, s62, v95
	v_med3_f32 v231, v231, s62, v95
	v_med3_f32 v232, v232, s62, v95
	v_med3_f32 v233, v233, s62, v95
	v_med3_f32 v234, v234, s62, v95
	v_med3_f32 v235, v235, s62, v95
	v_med3_f32 v236, v236, s62, v95
	v_med3_f32 v237, v237, s62, v95
	v_med3_f32 v238, v238, s62, v95
	v_med3_f32 v239, v239, s62, v95
	v_med3_f32 v240, v240, s62, v95
	v_med3_f32 v241, v241, s62, v95
	v_mov_b32_e32 v242, 0
	v_mov_b32_e32 v243, 0
	v_mov_b32_e32 v244, 0
	v_mov_b32_e32 v245, 0
	v_cvt_pk_fp8_f32 v242, v226, v227
	v_cvt_pk_fp8_f32 v243, v230, v231
	v_cvt_pk_fp8_f32 v244, v234, v235
	v_cvt_pk_fp8_f32 v245, v238, v239
	v_cvt_pk_fp8_f32 v242, v228, v229 op_sel:[0,0,1]
	v_cvt_pk_fp8_f32 v243, v232, v233 op_sel:[0,0,1]
	v_cvt_pk_fp8_f32 v244, v236, v237 op_sel:[0,0,1]
	v_cvt_pk_fp8_f32 v245, v240, v241 op_sel:[0,0,1]
	s_nop 0
	global_store_dwordx4 v77, v[242:245], s[6:7]
	ds_read_b32 v226, v214
	ds_read_b32 v227, v214 offset:512
	ds_read_b32 v228, v214 offset:1024
	ds_read_b32 v229, v214 offset:1536
	ds_read_b32 v230, v214 offset:2048
	ds_read_b32 v231, v214 offset:2560
	ds_read_b32 v232, v214 offset:3072
	ds_read_b32 v233, v214 offset:3584
	ds_read_b32 v234, v214 offset:4096
	ds_read_b32 v235, v214 offset:4608
	ds_read_b32 v236, v214 offset:5120
	ds_read_b32 v237, v214 offset:5632
	ds_read_b32 v238, v214 offset:6144
	ds_read_b32 v239, v214 offset:6656
	ds_read_b32 v240, v214 offset:7168
	ds_read_b32 v241, v214 offset:7680
	s_waitcnt lgkmcnt(0)
	v_max_f32_e32 v226, v226, v226
	v_max_f32_e32 v227, v227, v227
	v_max_f32_e32 v228, v228, v228
	v_max_f32_e32 v229, v229, v229
	v_max_f32_e32 v230, v230, v230
	v_max_f32_e32 v231, v231, v231
	v_max_f32_e32 v232, v232, v232
	v_max_f32_e32 v233, v233, v233
	v_max_f32_e32 v234, v234, v234
	v_max_f32_e32 v235, v235, v235
	v_max_f32_e32 v236, v236, v236
	v_max_f32_e32 v237, v237, v237
	v_max_f32_e32 v238, v238, v238
	v_max_f32_e32 v239, v239, v239
	v_max_f32_e32 v240, v240, v240
	v_max_f32_e32 v241, v241, v241
	v_med3_f32 v226, v226, s62, v95
	v_med3_f32 v227, v227, s62, v95
	v_med3_f32 v228, v228, s62, v95
	v_med3_f32 v229, v229, s62, v95
	v_med3_f32 v230, v230, s62, v95
	v_med3_f32 v231, v231, s62, v95
	v_med3_f32 v232, v232, s62, v95
	v_med3_f32 v233, v233, s62, v95
	v_med3_f32 v234, v234, s62, v95
	v_med3_f32 v235, v235, s62, v95
	v_med3_f32 v236, v236, s62, v95
	v_med3_f32 v237, v237, s62, v95
	v_med3_f32 v238, v238, s62, v95
	v_med3_f32 v239, v239, s62, v95
	v_med3_f32 v240, v240, s62, v95
	v_med3_f32 v241, v241, s62, v95
	v_mov_b32_e32 v242, 0
	v_mov_b32_e32 v243, 0
	v_mov_b32_e32 v244, 0
	v_mov_b32_e32 v245, 0
	v_cvt_pk_fp8_f32 v242, v226, v227
	v_cvt_pk_fp8_f32 v243, v230, v231
	v_cvt_pk_fp8_f32 v244, v234, v235
	v_cvt_pk_fp8_f32 v245, v238, v239
	v_cvt_pk_fp8_f32 v242, v228, v229 op_sel:[0,0,1]
	v_cvt_pk_fp8_f32 v243, v232, v233 op_sel:[0,0,1]
	v_cvt_pk_fp8_f32 v244, v236, v237 op_sel:[0,0,1]
	v_cvt_pk_fp8_f32 v245, v240, v241 op_sel:[0,0,1]
	s_nop 0
	global_store_dwordx4 v78, v[242:245], s[6:7]
	s_waitcnt vmcnt(12)
	v_mul_f32_e32 v144, v26, v144
	v_mul_f32_e32 v145, v26, v145
	v_mul_f32_e32 v146, v26, v146
	v_mul_f32_e32 v147, v26, v147
	ds_write_b128 v209, v[144:147]
	v_mul_f32_e32 v148, v27, v148
	v_mul_f32_e32 v149, v27, v149
	v_mul_f32_e32 v150, v27, v150
	v_mul_f32_e32 v151, v27, v151
	ds_write_b128 v209, v[148:151] offset:1024
	v_mul_f32_e32 v152, v28, v152
	v_mul_f32_e32 v153, v28, v153
	v_mul_f32_e32 v154, v28, v154
	v_mul_f32_e32 v155, v28, v155
	ds_write_b128 v209, v[152:155] offset:2048
	v_mul_f32_e32 v156, v29, v156
	v_mul_f32_e32 v157, v29, v157
	v_mul_f32_e32 v158, v29, v158
	v_mul_f32_e32 v159, v29, v159
	ds_write_b128 v209, v[156:159] offset:3072
	v_mul_f32_e32 v160, v30, v160
	v_mul_f32_e32 v161, v30, v161
	v_mul_f32_e32 v162, v30, v162
	v_mul_f32_e32 v163, v30, v163
	ds_write_b128 v209, v[160:163] offset:4096
	v_mul_f32_e32 v164, v31, v164
	v_mul_f32_e32 v165, v31, v165
	v_mul_f32_e32 v166, v31, v166
	v_mul_f32_e32 v167, v31, v167
	ds_write_b128 v209, v[164:167] offset:5120
	v_mul_f32_e32 v168, v32, v168
	v_mul_f32_e32 v169, v32, v169
	v_mul_f32_e32 v170, v32, v170
	v_mul_f32_e32 v171, v32, v171
	ds_write_b128 v209, v[168:171] offset:6144
	v_mul_f32_e32 v172, v33, v172
	v_mul_f32_e32 v173, v33, v173
	v_mul_f32_e32 v174, v33, v174
	v_mul_f32_e32 v175, v33, v175
	ds_write_b128 v209, v[172:175] offset:7168
	s_waitcnt lgkmcnt(0)
	s_barrier
; #define GAS __attribute__((address_space(1)))
; #define LAS __attribute__((address_space(3)))
; #define LDS_WAIT() asm volatile("s_waitcnt lgkmcnt(0)" ::: "memory")
; __device__ __forceinline__ unsigned pk4_fp8(float a, float b, float c, float d) {
;     a = fminf(fmaxf(a, -448.f), 448.f); b = fminf(fmaxf(b, -448.f), 448.f); c = fminf(fmaxf(c, -448.f), 448.f); d = fminf(fmaxf(d, -448.f), 448.f);
;     int w = __builtin_amdgcn_cvt_pk_fp8_f32(a, b, 0, false); w = __builtin_amdgcn_cvt_pk_fp8_f32(c, d, w, true); return (unsigned)w; }
;     const int pr = item >> 1, kb = 2 * (pr / nblk) + (item & 1), nb = pr % nblk, k0 = 64 * kb, n0 = 32 * nb;
;     const int nr = n0 + (lane & 31); const int sc = MAP == 1 ? src_col_in(nr) : nr;
;     float v[32];
; #pragma unroll
;     for (int i = 0; i < 32; ++i) v[i] = sc >= 0 ? W[(size_t)(k0 + 2 * i + (lane >> 5)) * Nsrc + sc] : 0.f;
; #pragma unroll
;     for (int i = 0; i < 32; ++i) { const int k = k0 + 2 * i + (lane >> 5); float x = v[i] * wscale; if (KS) x *= (k < ksplit ? ksA[k] : ksB[k - ksplit]); scr[(2 * i + (lane >> 5)) * 33 + (lane & 31)] = x; }
;     LDS_WAIT(); asm volatile("" ::: "memory");
;     const int c = lane & 7;
; #pragma unroll
;     for (int j = 0; j < 4; ++j) { const int n = (lane >> 3) + 8 * j; const LAS float* s = scr + (8 * c) * 33 + n;
;         const unsigned long long o = (unsigned long long)pg8::pk4_fp8(s[0 * 33], s[1 * 33], s[2 * 33], s[3 * 33]) | ((unsigned long long)pg8::pk4_fp8(s[4 * 33], s[5 * 33], s[6 * 33], s[7 * 33]) << 32);
;         *(GAS unsigned long long*)(WT + (size_t)(n0 + n) * K + k0 + 8 * c) = o; }
;     LDS_WAIT(); asm volatile("" ::: "memory");
	s_add_u32 s8, s30, 0x6000
	s_addc_u32 s9, s31, 0
	global_load_dwordx4 v[144:147], v74, s[8:9]
	s_add_u32 s8, s8, 0x20000
	s_addc_u32 s9, s9, 0
	global_load_dwordx4 v[148:151], v74, s[8:9]
	s_add_u32 s8, s8, 0x20000
	s_addc_u32 s9, s9, 0
	global_load_dwordx4 v[152:155], v74, s[8:9]
	s_add_u32 s8, s8, 0x20000
	s_addc_u32 s9, s9, 0
	global_load_dwordx4 v[156:159], v74, s[8:9]
	s_add_u32 s8, s8, 0x20000
	s_addc_u32 s9, s9, 0
	global_load_dwordx4 v[160:163], v74, s[8:9]
	s_add_u32 s8, s8, 0x20000
	s_addc_u32 s9, s9, 0
	global_load_dwordx4 v[164:167], v74, s[8:9]
	s_add_u32 s8, s8, 0x20000
	s_addc_u32 s9, s9, 0
	global_load_dwordx4 v[168:171], v74, s[8:9]
	s_add_u32 s8, s8, 0x20000
	s_addc_u32 s9, s9, 0
	global_load_dwordx4 v[172:175], v74, s[8:9]
	s_add_u32 s6, s32, 0x1000000
	s_addc_u32 s7, s33, 0
	ds_read_b32 v226, v211
	ds_read_b32 v227, v211 offset:512
	ds_read_b32 v228, v211 offset:1024
	ds_read_b32 v229, v211 offset:1536
	ds_read_b32 v230, v211 offset:2048
	ds_read_b32 v231, v211 offset:2560
	ds_read_b32 v232, v211 offset:3072
	ds_read_b32 v233, v211 offset:3584
	ds_read_b32 v234, v211 offset:4096
	ds_read_b32 v235, v211 offset:4608
	ds_read_b32 v236, v211 offset:5120
	ds_read_b32 v237, v211 offset:5632
	ds_read_b32 v238, v211 offset:6144
	ds_read_b32 v239, v211 offset:6656
	ds_read_b32 v240, v211 offset:7168
	ds_read_b32 v241, v211 offset:7680
	s_waitcnt lgkmcnt(0)
	v_max_f32_e32 v226, v226, v226
	v_max_f32_e32 v227, v227, v227
	v_max_f32_e32 v228, v228, v228
	v_max_f32_e32 v229, v229, v229
	v_max_f32_e32 v230, v230, v230
	v_max_f32_e32 v231, v231, v231
	v_max_f32_e32 v232, v232, v232
	v_max_f32_e32 v233, v233, v233
	v_max_f32_e32 v234, v234, v234
	v_max_f32_e32 v235, v235, v235
	v_max_f32_e32 v236, v236, v236
	v_max_f32_e32 v237, v237, v237
	v_max_f32_e32 v238, v238, v238
	v_max_f32_e32 v239, v239, v239
	v_max_f32_e32 v240, v240, v240
	v_max_f32_e32 v241, v241, v241
	v_med3_f32 v226, v226, s62, v95
	v_med3_f32 v227, v227, s62, v95
	v_med3_f32 v228, v228, s62, v95
	v_med3_f32 v229, v229, s62, v95
	v_med3_f32 v230, v230, s62, v95
	v_med3_f32 v231, v231, s62, v95
	v_med3_f32 v232, v232, s62, v95
	v_med3_f32 v233, v233, s62, v95
	v_med3_f32 v234, v234, s62, v95
	v_med3_f32 v235, v235, s62, v95
	v_med3_f32 v236, v236, s62, v95
	v_med3_f32 v237, v237, s62, v95
	v_med3_f32 v238, v238, s62, v95
	v_med3_f32 v239, v239, s62, v95
	v_med3_f32 v240, v240, s62, v95
	v_med3_f32 v241, v241, s62, v95
	v_mov_b32_e32 v242, 0
	v_mov_b32_e32 v243, 0
	v_mov_b32_e32 v244, 0
	v_mov_b32_e32 v245, 0
	v_cvt_pk_fp8_f32 v242, v226, v227
	v_cvt_pk_fp8_f32 v243, v230, v231
	v_cvt_pk_fp8_f32 v244, v234, v235
	v_cvt_pk_fp8_f32 v245, v238, v239
	v_cvt_pk_fp8_f32 v242, v228, v229 op_sel:[0,0,1]
	v_cvt_pk_fp8_f32 v243, v232, v233 op_sel:[0,0,1]
	v_cvt_pk_fp8_f32 v244, v236, v237 op_sel:[0,0,1]
	v_cvt_pk_fp8_f32 v245, v240, v241 op_sel:[0,0,1]
	s_nop 0
	global_store_dwordx4 v77, v[242:245], s[6:7]
	ds_read_b32 v226, v213
	ds_read_b32 v227, v213 offset:512
	ds_read_b32 v228, v213 offset:1024
	ds_read_b32 v229, v213 offset:1536
	ds_read_b32 v230, v213 offset:2048
	ds_read_b32 v231, v213 offset:2560
	ds_read_b32 v232, v213 offset:3072
	ds_read_b32 v233, v213 offset:3584
	ds_read_b32 v234, v213 offset:4096
	ds_read_b32 v235, v213 offset:4608
	ds_read_b32 v236, v213 offset:5120
	ds_read_b32 v237, v213 offset:5632
	ds_read_b32 v238, v213 offset:6144
	ds_read_b32 v239, v213 offset:6656
	ds_read_b32 v240, v213 offset:7168
	ds_read_b32 v241, v213 offset:7680
	s_waitcnt lgkmcnt(0)
	v_max_f32_e32 v226, v226, v226
	v_max_f32_e32 v227, v227, v227
	v_max_f32_e32 v228, v228, v228
	v_max_f32_e32 v229, v229, v229
	v_max_f32_e32 v230, v230, v230
	v_max_f32_e32 v231, v231, v231
	v_max_f32_e32 v232, v232, v232
	v_max_f32_e32 v233, v233, v233
	v_max_f32_e32 v234, v234, v234
	v_max_f32_e32 v235, v235, v235
	v_max_f32_e32 v236, v236, v236
	v_max_f32_e32 v237, v237, v237
	v_max_f32_e32 v238, v238, v238
	v_max_f32_e32 v239, v239, v239
	v_max_f32_e32 v240, v240, v240
	v_max_f32_e32 v241, v241, v241
	v_med3_f32 v226, v226, s62, v95
	v_med3_f32 v227, v227, s62, v95
	v_med3_f32 v228, v228, s62, v95
	v_med3_f32 v229, v229, s62, v95
	v_med3_f32 v230, v230, s62, v95
	v_med3_f32 v231, v231, s62, v95
	v_med3_f32 v232, v232, s62, v95
	v_med3_f32 v233, v233, s62, v95
	v_med3_f32 v234, v234, s62, v95
	v_med3_f32 v235, v235, s62, v95
	v_med3_f32 v236, v236, s62, v95
	v_med3_f32 v237, v237, s62, v95
	v_med3_f32 v238, v238, s62, v95
	v_med3_f32 v239, v239, s62, v95
	v_med3_f32 v240, v240, s62, v95
	v_med3_f32 v241, v241, s62, v95
	v_mov_b32_e32 v242, 0
	v_mov_b32_e32 v243, 0
	v_mov_b32_e32 v244, 0
	v_mov_b32_e32 v245, 0
	v_cvt_pk_fp8_f32 v242, v226, v227
	v_cvt_pk_fp8_f32 v243, v230, v231
	v_cvt_pk_fp8_f32 v244, v234, v235
	v_cvt_pk_fp8_f32 v245, v238, v239
	v_cvt_pk_fp8_f32 v242, v228, v229 op_sel:[0,0,1]
	v_cvt_pk_fp8_f32 v243, v232, v233 op_sel:[0,0,1]
	v_cvt_pk_fp8_f32 v244, v236, v237 op_sel:[0,0,1]
	v_cvt_pk_fp8_f32 v245, v240, v241 op_sel:[0,0,1]
	s_nop 0
	global_store_dwordx4 v78, v[242:245], s[6:7]
	s_waitcnt vmcnt(12)
	v_mul_f32_e32 v176, v26, v176
	v_mul_f32_e32 v177, v26, v177
	v_mul_f32_e32 v178, v26, v178
	v_mul_f32_e32 v179, v26, v179
	ds_write_b128 v210, v[176:179]
	v_mul_f32_e32 v180, v27, v180
	v_mul_f32_e32 v181, v27, v181
	v_mul_f32_e32 v182, v27, v182
	v_mul_f32_e32 v183, v27, v183
	ds_write_b128 v210, v[180:183] offset:1024
	v_mul_f32_e32 v184, v28, v184
	v_mul_f32_e32 v185, v28, v185
	v_mul_f32_e32 v186, v28, v186
	v_mul_f32_e32 v187, v28, v187
	ds_write_b128 v210, v[184:187] offset:2048
	v_mul_f32_e32 v188, v29, v188
	v_mul_f32_e32 v189, v29, v189
	v_mul_f32_e32 v190, v29, v190
	v_mul_f32_e32 v191, v29, v191
	ds_write_b128 v210, v[188:191] offset:3072
	v_mul_f32_e32 v192, v30, v192
	v_mul_f32_e32 v193, v30, v193
	v_mul_f32_e32 v194, v30, v194
	v_mul_f32_e32 v195, v30, v195
	ds_write_b128 v210, v[192:195] offset:4096
	v_mul_f32_e32 v196, v31, v196
	v_mul_f32_e32 v197, v31, v197
	v_mul_f32_e32 v198, v31, v198
	v_mul_f32_e32 v199, v31, v199
	ds_write_b128 v210, v[196:199] offset:5120
	v_mul_f32_e32 v200, v32, v200
	v_mul_f32_e32 v201, v32, v201
	v_mul_f32_e32 v202, v32, v202
	v_mul_f32_e32 v203, v32, v203
	ds_write_b128 v210, v[200:203] offset:6144
	v_mul_f32_e32 v204, v33, v204
	v_mul_f32_e32 v205, v33, v205
	v_mul_f32_e32 v206, v33, v206
	v_mul_f32_e32 v207, v33, v207
	ds_write_b128 v210, v[204:207] offset:7168
	s_waitcnt lgkmcnt(0)
	s_barrier
; #define GAS __attribute__((address_space(1)))
; #define LAS __attribute__((address_space(3)))
; #define LDS_WAIT() asm volatile("s_waitcnt lgkmcnt(0)" ::: "memory")
; __device__ __forceinline__ unsigned pk4_fp8(float a, float b, float c, float d) {
;     a = fminf(fmaxf(a, -448.f), 448.f); b = fminf(fmaxf(b, -448.f), 448.f); c = fminf(fmaxf(c, -448.f), 448.f); d = fminf(fmaxf(d, -448.f), 448.f);
;     int w = __builtin_amdgcn_cvt_pk_fp8_f32(a, b, 0, false); w = __builtin_amdgcn_cvt_pk_fp8_f32(c, d, w, true); return (unsigned)w; }
;     const int pr = item >> 1, kb = 2 * (pr / nblk) + (item & 1), nb = pr % nblk, k0 = 64 * kb, n0 = 32 * nb;
;     const int nr = n0 + (lane & 31); const int sc = MAP == 1 ? src_col_in(nr) : nr;
;     float v[32];
; #pragma unroll
;     for (int i = 0; i < 32; ++i) v[i] = sc >= 0 ? W[(size_t)(k0 + 2 * i + (lane >> 5)) * Nsrc + sc] : 0.f;
; #pragma unroll
;     for (int i = 0; i < 32; ++i) { const int k = k0 + 2 * i + (lane >> 5); float x = v[i] * wscale; if (KS) x *= (k < ksplit ? ksA[k] : ksB[k - ksplit]); scr[(2 * i + (lane >> 5)) * 33 + (lane & 31)] = x; }
;     LDS_WAIT(); asm volatile("" ::: "memory");
;     const int c = lane & 7;
; #pragma unroll
;     for (int j = 0; j < 4; ++j) { const int n = (lane >> 3) + 8 * j; const LAS float* s = scr + (8 * c) * 33 + n;
;         const unsigned long long o = (unsigned long long)pg8::pk4_fp8(s[0 * 33], s[1 * 33], s[2 * 33], s[3 * 33]) | ((unsigned long long)pg8::pk4_fp8(s[4 * 33], s[5 * 33], s[6 * 33], s[7 * 33]) << 32);
;         *(GAS unsigned long long*)(WT + (size_t)(n0 + n) * K + k0 + 8 * c) = o; }
;     LDS_WAIT(); asm volatile("" ::: "memory");
	s_add_u32 s8, s30, 0x7000
	s_addc_u32 s9, s31, 0
	global_load_dwordx4 v[176:179], v74, s[8:9]
	s_add_u32 s8, s8, 0x20000
	s_addc_u32 s9, s9, 0
	global_load_dwordx4 v[180:183], v74, s[8:9]
	s_add_u32 s8, s8, 0x20000
	s_addc_u32 s9, s9, 0
	global_load_dwordx4 v[184:187], v74, s[8:9]
	s_add_u32 s8, s8, 0x20000
	s_addc_u32 s9, s9, 0
	global_load_dwordx4 v[188:191], v74, s[8:9]
	s_add_u32 s8, s8, 0x20000
	s_addc_u32 s9, s9, 0
	global_load_dwordx4 v[192:195], v74, s[8:9]
	s_add_u32 s8, s8, 0x20000
	s_addc_u32 s9, s9, 0
	global_load_dwordx4 v[196:199], v74, s[8:9]
	s_add_u32 s8, s8, 0x20000
	s_addc_u32 s9, s9, 0
	global_load_dwordx4 v[200:203], v74, s[8:9]
	s_add_u32 s8, s8, 0x20000
	s_addc_u32 s9, s9, 0
	global_load_dwordx4 v[204:207], v74, s[8:9]
	s_add_u32 s6, s32, 0x1400000
	s_addc_u32 s7, s33, 0
	ds_read_b32 v226, v212
	ds_read_b32 v227, v212 offset:512
	ds_read_b32 v228, v212 offset:1024
	ds_read_b32 v229, v212 offset:1536
	ds_read_b32 v230, v212 offset:2048
	ds_read_b32 v231, v212 offset:2560
	ds_read_b32 v232, v212 offset:3072
	ds_read_b32 v233, v212 offset:3584
	ds_read_b32 v234, v212 offset:4096
	ds_read_b32 v235, v212 offset:4608
	ds_read_b32 v236, v212 offset:5120
	ds_read_b32 v237, v212 offset:5632
	ds_read_b32 v238, v212 offset:6144
	ds_read_b32 v239, v212 offset:6656
	ds_read_b32 v240, v212 offset:7168
	ds_read_b32 v241, v212 offset:7680
	s_waitcnt lgkmcnt(0)
	v_max_f32_e32 v226, v226, v226
	v_max_f32_e32 v227, v227, v227
	v_max_f32_e32 v228, v228, v228
	v_max_f32_e32 v229, v229, v229
	v_max_f32_e32 v230, v230, v230
	v_max_f32_e32 v231, v231, v231
	v_max_f32_e32 v232, v232, v232
	v_max_f32_e32 v233, v233, v233
	v_max_f32_e32 v234, v234, v234
	v_max_f32_e32 v235, v235, v235
	v_max_f32_e32 v236, v236, v236
	v_max_f32_e32 v237, v237, v237
	v_max_f32_e32 v238, v238, v238
	v_max_f32_e32 v239, v239, v239
	v_max_f32_e32 v240, v240, v240
	v_max_f32_e32 v241, v241, v241
	v_med3_f32 v226, v226, s62, v95
	v_med3_f32 v227, v227, s62, v95
	v_med3_f32 v228, v228, s62, v95
	v_med3_f32 v229, v229, s62, v95
	v_med3_f32 v230, v230, s62, v95
	v_med3_f32 v231, v231, s62, v95
	v_med3_f32 v232, v232, s62, v95
	v_med3_f32 v233, v233, s62, v95
	v_med3_f32 v234, v234, s62, v95
	v_med3_f32 v235, v235, s62, v95
	v_med3_f32 v236, v236, s62, v95
	v_med3_f32 v237, v237, s62, v95
	v_med3_f32 v238, v238, s62, v95
	v_med3_f32 v239, v239, s62, v95
	v_med3_f32 v240, v240, s62, v95
	v_med3_f32 v241, v241, s62, v95
	v_mov_b32_e32 v242, 0
	v_mov_b32_e32 v243, 0
	v_mov_b32_e32 v244, 0
	v_mov_b32_e32 v245, 0
	v_cvt_pk_fp8_f32 v242, v226, v227
	v_cvt_pk_fp8_f32 v243, v230, v231
	v_cvt_pk_fp8_f32 v244, v234, v235
	v_cvt_pk_fp8_f32 v245, v238, v239
	v_cvt_pk_fp8_f32 v242, v228, v229 op_sel:[0,0,1]
	v_cvt_pk_fp8_f32 v243, v232, v233 op_sel:[0,0,1]
	v_cvt_pk_fp8_f32 v244, v236, v237 op_sel:[0,0,1]
	v_cvt_pk_fp8_f32 v245, v240, v241 op_sel:[0,0,1]
	s_nop 0
	global_store_dwordx4 v77, v[242:245], s[6:7]
	ds_read_b32 v226, v214
	ds_read_b32 v227, v214 offset:512
	ds_read_b32 v228, v214 offset:1024
	ds_read_b32 v229, v214 offset:1536
	ds_read_b32 v230, v214 offset:2048
	ds_read_b32 v231, v214 offset:2560
	ds_read_b32 v232, v214 offset:3072
	ds_read_b32 v233, v214 offset:3584
	ds_read_b32 v234, v214 offset:4096
	ds_read_b32 v235, v214 offset:4608
	ds_read_b32 v236, v214 offset:5120
	ds_read_b32 v237, v214 offset:5632
	ds_read_b32 v238, v214 offset:6144
	ds_read_b32 v239, v214 offset:6656
	ds_read_b32 v240, v214 offset:7168
	ds_read_b32 v241, v214 offset:7680
	s_waitcnt lgkmcnt(0)
	v_max_f32_e32 v226, v226, v226
	v_max_f32_e32 v227, v227, v227
	v_max_f32_e32 v228, v228, v228
	v_max_f32_e32 v229, v229, v229
	v_max_f32_e32 v230, v230, v230
	v_max_f32_e32 v231, v231, v231
	v_max_f32_e32 v232, v232, v232
	v_max_f32_e32 v233, v233, v233
	v_max_f32_e32 v234, v234, v234
	v_max_f32_e32 v235, v235, v235
	v_max_f32_e32 v236, v236, v236
	v_max_f32_e32 v237, v237, v237
	v_max_f32_e32 v238, v238, v238
	v_max_f32_e32 v239, v239, v239
	v_max_f32_e32 v240, v240, v240
	v_max_f32_e32 v241, v241, v241
	v_med3_f32 v226, v226, s62, v95
	v_med3_f32 v227, v227, s62, v95
	v_med3_f32 v228, v228, s62, v95
	v_med3_f32 v229, v229, s62, v95
	v_med3_f32 v230, v230, s62, v95
	v_med3_f32 v231, v231, s62, v95
	v_med3_f32 v232, v232, s62, v95
	v_med3_f32 v233, v233, s62, v95
	v_med3_f32 v234, v234, s62, v95
	v_med3_f32 v235, v235, s62, v95
	v_med3_f32 v236, v236, s62, v95
	v_med3_f32 v237, v237, s62, v95
	v_med3_f32 v238, v238, s62, v95
	v_med3_f32 v239, v239, s62, v95
	v_med3_f32 v240, v240, s62, v95
	v_med3_f32 v241, v241, s62, v95
	v_mov_b32_e32 v242, 0
	v_mov_b32_e32 v243, 0
	v_mov_b32_e32 v244, 0
	v_mov_b32_e32 v245, 0
	v_cvt_pk_fp8_f32 v242, v226, v227
	v_cvt_pk_fp8_f32 v243, v230, v231
	v_cvt_pk_fp8_f32 v244, v234, v235
	v_cvt_pk_fp8_f32 v245, v238, v239
	v_cvt_pk_fp8_f32 v242, v228, v229 op_sel:[0,0,1]
	v_cvt_pk_fp8_f32 v243, v232, v233 op_sel:[0,0,1]
	v_cvt_pk_fp8_f32 v244, v236, v237 op_sel:[0,0,1]
	v_cvt_pk_fp8_f32 v245, v240, v241 op_sel:[0,0,1]
	s_nop 0
	global_store_dwordx4 v78, v[242:245], s[6:7]
	s_waitcnt vmcnt(12)
	v_mul_f32_e32 v144, v26, v144
	v_mul_f32_e32 v145, v26, v145
	v_mul_f32_e32 v146, v26, v146
	v_mul_f32_e32 v147, v26, v147
	ds_write_b128 v209, v[144:147]
	v_mul_f32_e32 v148, v27, v148
	v_mul_f32_e32 v149, v27, v149
	v_mul_f32_e32 v150, v27, v150
	v_mul_f32_e32 v151, v27, v151
	ds_write_b128 v209, v[148:151] offset:1024
	v_mul_f32_e32 v152, v28, v152
	v_mul_f32_e32 v153, v28, v153
	v_mul_f32_e32 v154, v28, v154
	v_mul_f32_e32 v155, v28, v155
	ds_write_b128 v209, v[152:155] offset:2048
	v_mul_f32_e32 v156, v29, v156
	v_mul_f32_e32 v157, v29, v157
	v_mul_f32_e32 v158, v29, v158
	v_mul_f32_e32 v159, v29, v159
	ds_write_b128 v209, v[156:159] offset:3072
	v_mul_f32_e32 v160, v30, v160
	v_mul_f32_e32 v161, v30, v161
	v_mul_f32_e32 v162, v30, v162
	v_mul_f32_e32 v163, v30, v163
	ds_write_b128 v209, v[160:163] offset:4096
	v_mul_f32_e32 v164, v31, v164
	v_mul_f32_e32 v165, v31, v165
	v_mul_f32_e32 v166, v31, v166
	v_mul_f32_e32 v167, v31, v167
	ds_write_b128 v209, v[164:167] offset:5120
	v_mul_f32_e32 v168, v32, v168
	v_mul_f32_e32 v169, v32, v169
	v_mul_f32_e32 v170, v32, v170
	v_mul_f32_e32 v171, v32, v171
	ds_write_b128 v209, v[168:171] offset:6144
	v_mul_f32_e32 v172, v33, v172
	v_mul_f32_e32 v173, v33, v173
	v_mul_f32_e32 v174, v33, v174
	v_mul_f32_e32 v175, v33, v175
	ds_write_b128 v209, v[172:175] offset:7168
	s_waitcnt lgkmcnt(0)
	s_barrier
; #define GAS __attribute__((address_space(1)))
; #define LAS __attribute__((address_space(3)))
; #define LDS_WAIT() asm volatile("s_waitcnt lgkmcnt(0)" ::: "memory")
; __device__ __forceinline__ unsigned pk4_fp8(float a, float b, float c, float d) {
;     a = fminf(fmaxf(a, -448.f), 448.f); b = fminf(fmaxf(b, -448.f), 448.f); c = fminf(fmaxf(c, -448.f), 448.f); d = fminf(fmaxf(d, -448.f), 448.f);
;     int w = __builtin_amdgcn_cvt_pk_fp8_f32(a, b, 0, false); w = __builtin_amdgcn_cvt_pk_fp8_f32(c, d, w, true); return (unsigned)w; }
;     const int pr = item >> 1, kb = 2 * (pr / nblk) + (item & 1), nb = pr % nblk, k0 = 64 * kb, n0 = 32 * nb;
;     const int nr = n0 + (lane & 31); const int sc = MAP == 1 ? src_col_in(nr) : nr;
;     float v[32];
; #pragma unroll
;     for (int i = 0; i < 32; ++i) v[i] = sc >= 0 ? W[(size_t)(k0 + 2 * i + (lane >> 5)) * Nsrc + sc] : 0.f;
; #pragma unroll
;     for (int i = 0; i < 32; ++i) { const int k = k0 + 2 * i + (lane >> 5); float x = v[i] * wscale; if (KS) x *= (k < ksplit ? ksA[k] : ksB[k - ksplit]); scr[(2 * i + (lane >> 5)) * 33 + (lane & 31)] = x; }
;     LDS_WAIT(); asm volatile("" ::: "memory");
;     const int c = lane & 7;
; #pragma unroll
;     for (int j = 0; j < 4; ++j) { const int n = (lane >> 3) + 8 * j; const LAS float* s = scr + (8 * c) * 33 + n;
;         const unsigned long long o = (unsigned long long)pg8::pk4_fp8(s[0 * 33], s[1 * 33], s[2 * 33], s[3 * 33]) | ((unsigned long long)pg8::pk4_fp8(s[4 * 33], s[5 * 33], s[6 * 33], s[7 * 33]) << 32);
;         *(GAS unsigned long long*)(WT + (size_t)(n0 + n) * K + k0 + 8 * c) = o; }
;     LDS_WAIT(); asm volatile("" ::: "memory");
	s_add_u32 s8, s30, 0x8000
	s_addc_u32 s9, s31, 0
	global_load_dwordx4 v[144:147], v74, s[8:9]
	s_add_u32 s8, s8, 0x20000
	s_addc_u32 s9, s9, 0
	global_load_dwordx4 v[148:151], v74, s[8:9]
	s_add_u32 s8, s8, 0x20000
	s_addc_u32 s9, s9, 0
	global_load_dwordx4 v[152:155], v74, s[8:9]
	s_add_u32 s8, s8, 0x20000
	s_addc_u32 s9, s9, 0
	global_load_dwordx4 v[156:159], v74, s[8:9]
	s_add_u32 s8, s8, 0x20000
	s_addc_u32 s9, s9, 0
	global_load_dwordx4 v[160:163], v74, s[8:9]
	s_add_u32 s8, s8, 0x20000
	s_addc_u32 s9, s9, 0
	global_load_dwordx4 v[164:167], v74, s[8:9]
	s_add_u32 s8, s8, 0x20000
	s_addc_u32 s9, s9, 0
	global_load_dwordx4 v[168:171], v74, s[8:9]
	s_add_u32 s8, s8, 0x20000
	s_addc_u32 s9, s9, 0
	global_load_dwordx4 v[172:175], v74, s[8:9]
	s_add_u32 s6, s32, 0x1800000
	s_addc_u32 s7, s33, 0
	ds_read_b32 v226, v211
	ds_read_b32 v227, v211 offset:512
	ds_read_b32 v228, v211 offset:1024
	ds_read_b32 v229, v211 offset:1536
	ds_read_b32 v230, v211 offset:2048
	ds_read_b32 v231, v211 offset:2560
	ds_read_b32 v232, v211 offset:3072
	ds_read_b32 v233, v211 offset:3584
	ds_read_b32 v234, v211 offset:4096
	ds_read_b32 v235, v211 offset:4608
	ds_read_b32 v236, v211 offset:5120
	ds_read_b32 v237, v211 offset:5632
	ds_read_b32 v238, v211 offset:6144
	ds_read_b32 v239, v211 offset:6656
	ds_read_b32 v240, v211 offset:7168
	ds_read_b32 v241, v211 offset:7680
	s_waitcnt lgkmcnt(0)
	v_max_f32_e32 v226, v226, v226
	v_max_f32_e32 v227, v227, v227
	v_max_f32_e32 v228, v228, v228
	v_max_f32_e32 v229, v229, v229
	v_max_f32_e32 v230, v230, v230
	v_max_f32_e32 v231, v231, v231
	v_max_f32_e32 v232, v232, v232
	v_max_f32_e32 v233, v233, v233
	v_max_f32_e32 v234, v234, v234
	v_max_f32_e32 v235, v235, v235
	v_max_f32_e32 v236, v236, v236
	v_max_f32_e32 v237, v237, v237
	v_max_f32_e32 v238, v238, v238
	v_max_f32_e32 v239, v239, v239
	v_max_f32_e32 v240, v240, v240
	v_max_f32_e32 v241, v241, v241
	v_med3_f32 v226, v226, s62, v95
	v_med3_f32 v227, v227, s62, v95
	v_med3_f32 v228, v228, s62, v95
	v_med3_f32 v229, v229, s62, v95
	v_med3_f32 v230, v230, s62, v95
	v_med3_f32 v231, v231, s62, v95
	v_med3_f32 v232, v232, s62, v95
	v_med3_f32 v233, v233, s62, v95
	v_med3_f32 v234, v234, s62, v95
	v_med3_f32 v235, v235, s62, v95
	v_med3_f32 v236, v236, s62, v95
	v_med3_f32 v237, v237, s62, v95
	v_med3_f32 v238, v238, s62, v95
	v_med3_f32 v239, v239, s62, v95
	v_med3_f32 v240, v240, s62, v95
	v_med3_f32 v241, v241, s62, v95
	v_mov_b32_e32 v242, 0
	v_mov_b32_e32 v243, 0
	v_mov_b32_e32 v244, 0
	v_mov_b32_e32 v245, 0
	v_cvt_pk_fp8_f32 v242, v226, v227
	v_cvt_pk_fp8_f32 v243, v230, v231
	v_cvt_pk_fp8_f32 v244, v234, v235
	v_cvt_pk_fp8_f32 v245, v238, v239
	v_cvt_pk_fp8_f32 v242, v228, v229 op_sel:[0,0,1]
	v_cvt_pk_fp8_f32 v243, v232, v233 op_sel:[0,0,1]
	v_cvt_pk_fp8_f32 v244, v236, v237 op_sel:[0,0,1]
	v_cvt_pk_fp8_f32 v245, v240, v241 op_sel:[0,0,1]
	s_nop 0
	global_store_dwordx4 v77, v[242:245], s[6:7]
	ds_read_b32 v226, v213
	ds_read_b32 v227, v213 offset:512
	ds_read_b32 v228, v213 offset:1024
	ds_read_b32 v229, v213 offset:1536
	ds_read_b32 v230, v213 offset:2048
	ds_read_b32 v231, v213 offset:2560
	ds_read_b32 v232, v213 offset:3072
	ds_read_b32 v233, v213 offset:3584
	ds_read_b32 v234, v213 offset:4096
	ds_read_b32 v235, v213 offset:4608
	ds_read_b32 v236, v213 offset:5120
	ds_read_b32 v237, v213 offset:5632
	ds_read_b32 v238, v213 offset:6144
	ds_read_b32 v239, v213 offset:6656
	ds_read_b32 v240, v213 offset:7168
	ds_read_b32 v241, v213 offset:7680
	s_waitcnt lgkmcnt(0)
	v_max_f32_e32 v226, v226, v226
	v_max_f32_e32 v227, v227, v227
	v_max_f32_e32 v228, v228, v228
	v_max_f32_e32 v229, v229, v229
	v_max_f32_e32 v230, v230, v230
	v_max_f32_e32 v231, v231, v231
	v_max_f32_e32 v232, v232, v232
	v_max_f32_e32 v233, v233, v233
	v_max_f32_e32 v234, v234, v234
	v_max_f32_e32 v235, v235, v235
	v_max_f32_e32 v236, v236, v236
	v_max_f32_e32 v237, v237, v237
	v_max_f32_e32 v238, v238, v238
	v_max_f32_e32 v239, v239, v239
	v_max_f32_e32 v240, v240, v240
	v_max_f32_e32 v241, v241, v241
	v_med3_f32 v226, v226, s62, v95
	v_med3_f32 v227, v227, s62, v95
	v_med3_f32 v228, v228, s62, v95
	v_med3_f32 v229, v229, s62, v95
	v_med3_f32 v230, v230, s62, v95
	v_med3_f32 v231, v231, s62, v95
	v_med3_f32 v232, v232, s62, v95
	v_med3_f32 v233, v233, s62, v95
	v_med3_f32 v234, v234, s62, v95
	v_med3_f32 v235, v235, s62, v95
	v_med3_f32 v236, v236, s62, v95
	v_med3_f32 v237, v237, s62, v95
	v_med3_f32 v238, v238, s62, v95
	v_med3_f32 v239, v239, s62, v95
	v_med3_f32 v240, v240, s62, v95
	v_med3_f32 v241, v241, s62, v95
	v_mov_b32_e32 v242, 0
	v_mov_b32_e32 v243, 0
	v_mov_b32_e32 v244, 0
	v_mov_b32_e32 v245, 0
	v_cvt_pk_fp8_f32 v242, v226, v227
	v_cvt_pk_fp8_f32 v243, v230, v231
	v_cvt_pk_fp8_f32 v244, v234, v235
	v_cvt_pk_fp8_f32 v245, v238, v239
	v_cvt_pk_fp8_f32 v242, v228, v229 op_sel:[0,0,1]
	v_cvt_pk_fp8_f32 v243, v232, v233 op_sel:[0,0,1]
	v_cvt_pk_fp8_f32 v244, v236, v237 op_sel:[0,0,1]
	v_cvt_pk_fp8_f32 v245, v240, v241 op_sel:[0,0,1]
	s_nop 0
	global_store_dwordx4 v78, v[242:245], s[6:7]
	s_waitcnt vmcnt(12)
	v_mul_f32_e32 v176, v26, v176
	v_mul_f32_e32 v177, v26, v177
	v_mul_f32_e32 v178, v26, v178
	v_mul_f32_e32 v179, v26, v179
	ds_write_b128 v210, v[176:179]
	v_mul_f32_e32 v180, v27, v180
	v_mul_f32_e32 v181, v27, v181
	v_mul_f32_e32 v182, v27, v182
	v_mul_f32_e32 v183, v27, v183
	ds_write_b128 v210, v[180:183] offset:1024
	v_mul_f32_e32 v184, v28, v184
	v_mul_f32_e32 v185, v28, v185
	v_mul_f32_e32 v186, v28, v186
	v_mul_f32_e32 v187, v28, v187
	ds_write_b128 v210, v[184:187] offset:2048
	v_mul_f32_e32 v188, v29, v188
	v_mul_f32_e32 v189, v29, v189
	v_mul_f32_e32 v190, v29, v190
	v_mul_f32_e32 v191, v29, v191
	ds_write_b128 v210, v[188:191] offset:3072
	v_mul_f32_e32 v192, v30, v192
	v_mul_f32_e32 v193, v30, v193
	v_mul_f32_e32 v194, v30, v194
	v_mul_f32_e32 v195, v30, v195
	ds_write_b128 v210, v[192:195] offset:4096
	v_mul_f32_e32 v196, v31, v196
	v_mul_f32_e32 v197, v31, v197
	v_mul_f32_e32 v198, v31, v198
	v_mul_f32_e32 v199, v31, v199
	ds_write_b128 v210, v[196:199] offset:5120
	v_mul_f32_e32 v200, v32, v200
	v_mul_f32_e32 v201, v32, v201
	v_mul_f32_e32 v202, v32, v202
	v_mul_f32_e32 v203, v32, v203
	ds_write_b128 v210, v[200:203] offset:6144
	v_mul_f32_e32 v204, v33, v204
	v_mul_f32_e32 v205, v33, v205
	v_mul_f32_e32 v206, v33, v206
	v_mul_f32_e32 v207, v33, v207
	ds_write_b128 v210, v[204:207] offset:7168
	s_waitcnt lgkmcnt(0)
	s_barrier
; #define GAS __attribute__((address_space(1)))
; #define LAS __attribute__((address_space(3)))
; #define LDS_WAIT() asm volatile("s_waitcnt lgkmcnt(0)" ::: "memory")
; __device__ __forceinline__ unsigned pk4_fp8(float a, float b, float c, float d) {
;     a = fminf(fmaxf(a, -448.f), 448.f); b = fminf(fmaxf(b, -448.f), 448.f); c = fminf(fmaxf(c, -448.f), 448.f); d = fminf(fmaxf(d, -448.f), 448.f);
;     int w = __builtin_amdgcn_cvt_pk_fp8_f32(a, b, 0, false); w = __builtin_amdgcn_cvt_pk_fp8_f32(c, d, w, true); return (unsigned)w; }
;     const int pr = item >> 1, kb = 2 * (pr / nblk) + (item & 1), nb = pr % nblk, k0 = 64 * kb, n0 = 32 * nb;
;     const int nr = n0 + (lane & 31); const int sc = MAP == 1 ? src_col_in(nr) : nr;
;     float v[32];
; #pragma unroll
;     for (int i = 0; i < 32; ++i) v[i] = sc >= 0 ? W[(size_t)(k0 + 2 * i + (lane >> 5)) * Nsrc + sc] : 0.f;
; #pragma unroll
;     for (int i = 0; i < 32; ++i) { const int k = k0 + 2 * i + (lane >> 5); float x = v[i] * wscale; if (KS) x *= (k < ksplit ? ksA[k] : ksB[k - ksplit]); scr[(2 * i + (lane >> 5)) * 33 + (lane & 31)] = x; }
;     LDS_WAIT(); asm volatile("" ::: "memory");
;     const int c = lane & 7;
; #pragma unroll
;     for (int j = 0; j < 4; ++j) { const int n = (lane >> 3) + 8 * j; const LAS float* s = scr + (8 * c) * 33 + n;
;         const unsigned long long o = (unsigned long long)pg8::pk4_fp8(s[0 * 33], s[1 * 33], s[2 * 33], s[3 * 33]) | ((unsigned long long)pg8::pk4_fp8(s[4 * 33], s[5 * 33], s[6 * 33], s[7 * 33]) << 32);
;         *(GAS unsigned long long*)(WT + (size_t)(n0 + n) * K + k0 + 8 * c) = o; }
;     LDS_WAIT(); asm volatile("" ::: "memory");
	s_add_u32 s8, s30, 0x9000
	s_addc_u32 s9, s31, 0
	global_load_dwordx4 v[176:179], v74, s[8:9]
	s_add_u32 s8, s8, 0x20000
	s_addc_u32 s9, s9, 0
	global_load_dwordx4 v[180:183], v74, s[8:9]
	s_add_u32 s8, s8, 0x20000
	s_addc_u32 s9, s9, 0
	global_load_dwordx4 v[184:187], v74, s[8:9]
	s_add_u32 s8, s8, 0x20000
	s_addc_u32 s9, s9, 0
	global_load_dwordx4 v[188:191], v74, s[8:9]
	s_add_u32 s8, s8, 0x20000
	s_addc_u32 s9, s9, 0
	global_load_dwordx4 v[192:195], v74, s[8:9]
	s_add_u32 s8, s8, 0x20000
	s_addc_u32 s9, s9, 0
	global_load_dwordx4 v[196:199], v74, s[8:9]
	s_add_u32 s8, s8, 0x20000
	s_addc_u32 s9, s9, 0
	global_load_dwordx4 v[200:203], v74, s[8:9]
	s_add_u32 s8, s8, 0x20000
	s_addc_u32 s9, s9, 0
	global_load_dwordx4 v[204:207], v74, s[8:9]
	s_add_u32 s6, s32, 0x1c00000
	s_addc_u32 s7, s33, 0
	ds_read_b32 v226, v212
	ds_read_b32 v227, v212 offset:512
	ds_read_b32 v228, v212 offset:1024
	ds_read_b32 v229, v212 offset:1536
	ds_read_b32 v230, v212 offset:2048
	ds_read_b32 v231, v212 offset:2560
	ds_read_b32 v232, v212 offset:3072
	ds_read_b32 v233, v212 offset:3584
	ds_read_b32 v234, v212 offset:4096
	ds_read_b32 v235, v212 offset:4608
	ds_read_b32 v236, v212 offset:5120
	ds_read_b32 v237, v212 offset:5632
	ds_read_b32 v238, v212 offset:6144
	ds_read_b32 v239, v212 offset:6656
	ds_read_b32 v240, v212 offset:7168
	ds_read_b32 v241, v212 offset:7680
	s_waitcnt lgkmcnt(0)
	v_max_f32_e32 v226, v226, v226
	v_max_f32_e32 v227, v227, v227
	v_max_f32_e32 v228, v228, v228
	v_max_f32_e32 v229, v229, v229
	v_max_f32_e32 v230, v230, v230
	v_max_f32_e32 v231, v231, v231
	v_max_f32_e32 v232, v232, v232
	v_max_f32_e32 v233, v233, v233
	v_max_f32_e32 v234, v234, v234
	v_max_f32_e32 v235, v235, v235
	v_max_f32_e32 v236, v236, v236
	v_max_f32_e32 v237, v237, v237
	v_max_f32_e32 v238, v238, v238
	v_max_f32_e32 v239, v239, v239
	v_max_f32_e32 v240, v240, v240
	v_max_f32_e32 v241, v241, v241
	v_med3_f32 v226, v226, s62, v95
	v_med3_f32 v227, v227, s62, v95
	v_med3_f32 v228, v228, s62, v95
	v_med3_f32 v229, v229, s62, v95
	v_med3_f32 v230, v230, s62, v95
	v_med3_f32 v231, v231, s62, v95
	v_med3_f32 v232, v232, s62, v95
	v_med3_f32 v233, v233, s62, v95
	v_med3_f32 v234, v234, s62, v95
	v_med3_f32 v235, v235, s62, v95
	v_med3_f32 v236, v236, s62, v95
	v_med3_f32 v237, v237, s62, v95
	v_med3_f32 v238, v238, s62, v95
	v_med3_f32 v239, v239, s62, v95
	v_med3_f32 v240, v240, s62, v95
	v_med3_f32 v241, v241, s62, v95
	v_mov_b32_e32 v242, 0
	v_mov_b32_e32 v243, 0
	v_mov_b32_e32 v244, 0
	v_mov_b32_e32 v245, 0
	v_cvt_pk_fp8_f32 v242, v226, v227
	v_cvt_pk_fp8_f32 v243, v230, v231
	v_cvt_pk_fp8_f32 v244, v234, v235
	v_cvt_pk_fp8_f32 v245, v238, v239
	v_cvt_pk_fp8_f32 v242, v228, v229 op_sel:[0,0,1]
	v_cvt_pk_fp8_f32 v243, v232, v233 op_sel:[0,0,1]
	v_cvt_pk_fp8_f32 v244, v236, v237 op_sel:[0,0,1]
	v_cvt_pk_fp8_f32 v245, v240, v241 op_sel:[0,0,1]
	s_nop 0
	global_store_dwordx4 v77, v[242:245], s[6:7]
	ds_read_b32 v226, v214
	ds_read_b32 v227, v214 offset:512
	ds_read_b32 v228, v214 offset:1024
	ds_read_b32 v229, v214 offset:1536
	ds_read_b32 v230, v214 offset:2048
	ds_read_b32 v231, v214 offset:2560
	ds_read_b32 v232, v214 offset:3072
	ds_read_b32 v233, v214 offset:3584
	ds_read_b32 v234, v214 offset:4096
	ds_read_b32 v235, v214 offset:4608
	ds_read_b32 v236, v214 offset:5120
	ds_read_b32 v237, v214 offset:5632
	ds_read_b32 v238, v214 offset:6144
	ds_read_b32 v239, v214 offset:6656
	ds_read_b32 v240, v214 offset:7168
	ds_read_b32 v241, v214 offset:7680
	s_waitcnt lgkmcnt(0)
	v_max_f32_e32 v226, v226, v226
	v_max_f32_e32 v227, v227, v227
	v_max_f32_e32 v228, v228, v228
	v_max_f32_e32 v229, v229, v229
	v_max_f32_e32 v230, v230, v230
	v_max_f32_e32 v231, v231, v231
	v_max_f32_e32 v232, v232, v232
	v_max_f32_e32 v233, v233, v233
	v_max_f32_e32 v234, v234, v234
	v_max_f32_e32 v235, v235, v235
	v_max_f32_e32 v236, v236, v236
	v_max_f32_e32 v237, v237, v237
	v_max_f32_e32 v238, v238, v238
	v_max_f32_e32 v239, v239, v239
	v_max_f32_e32 v240, v240, v240
	v_max_f32_e32 v241, v241, v241
	v_med3_f32 v226, v226, s62, v95
	v_med3_f32 v227, v227, s62, v95
	v_med3_f32 v228, v228, s62, v95
	v_med3_f32 v229, v229, s62, v95
	v_med3_f32 v230, v230, s62, v95
	v_med3_f32 v231, v231, s62, v95
	v_med3_f32 v232, v232, s62, v95
	v_med3_f32 v233, v233, s62, v95
	v_med3_f32 v234, v234, s62, v95
	v_med3_f32 v235, v235, s62, v95
	v_med3_f32 v236, v236, s62, v95
	v_med3_f32 v237, v237, s62, v95
	v_med3_f32 v238, v238, s62, v95
	v_med3_f32 v239, v239, s62, v95
	v_med3_f32 v240, v240, s62, v95
	v_med3_f32 v241, v241, s62, v95
	v_mov_b32_e32 v242, 0
	v_mov_b32_e32 v243, 0
	v_mov_b32_e32 v244, 0
	v_mov_b32_e32 v245, 0
	v_cvt_pk_fp8_f32 v242, v226, v227
	v_cvt_pk_fp8_f32 v243, v230, v231
	v_cvt_pk_fp8_f32 v244, v234, v235
	v_cvt_pk_fp8_f32 v245, v238, v239
	v_cvt_pk_fp8_f32 v242, v228, v229 op_sel:[0,0,1]
	v_cvt_pk_fp8_f32 v243, v232, v233 op_sel:[0,0,1]
	v_cvt_pk_fp8_f32 v244, v236, v237 op_sel:[0,0,1]
	v_cvt_pk_fp8_f32 v245, v240, v241 op_sel:[0,0,1]
	s_nop 0
	global_store_dwordx4 v78, v[242:245], s[6:7]
	s_waitcnt vmcnt(12)
	v_mul_f32_e32 v144, v26, v144
	v_mul_f32_e32 v145, v26, v145
	v_mul_f32_e32 v146, v26, v146
	v_mul_f32_e32 v147, v26, v147
	ds_write_b128 v209, v[144:147]
	v_mul_f32_e32 v148, v27, v148
	v_mul_f32_e32 v149, v27, v149
	v_mul_f32_e32 v150, v27, v150
	v_mul_f32_e32 v151, v27, v151
	ds_write_b128 v209, v[148:151] offset:1024
	v_mul_f32_e32 v152, v28, v152
	v_mul_f32_e32 v153, v28, v153
	v_mul_f32_e32 v154, v28, v154
	v_mul_f32_e32 v155, v28, v155
	ds_write_b128 v209, v[152:155] offset:2048
	v_mul_f32_e32 v156, v29, v156
	v_mul_f32_e32 v157, v29, v157
	v_mul_f32_e32 v158, v29, v158
	v_mul_f32_e32 v159, v29, v159
	ds_write_b128 v209, v[156:159] offset:3072
	v_mul_f32_e32 v160, v30, v160
	v_mul_f32_e32 v161, v30, v161
	v_mul_f32_e32 v162, v30, v162
	v_mul_f32_e32 v163, v30, v163
	ds_write_b128 v209, v[160:163] offset:4096
	v_mul_f32_e32 v164, v31, v164
	v_mul_f32_e32 v165, v31, v165
	v_mul_f32_e32 v166, v31, v166
	v_mul_f32_e32 v167, v31, v167
	ds_write_b128 v209, v[164:167] offset:5120
	v_mul_f32_e32 v168, v32, v168
	v_mul_f32_e32 v169, v32, v169
	v_mul_f32_e32 v170, v32, v170
	v_mul_f32_e32 v171, v32, v171
	ds_write_b128 v209, v[168:171] offset:6144
	v_mul_f32_e32 v172, v33, v172
	v_mul_f32_e32 v173, v33, v173
	v_mul_f32_e32 v174, v33, v174
	v_mul_f32_e32 v175, v33, v175
	ds_write_b128 v209, v[172:175] offset:7168
	s_waitcnt lgkmcnt(0)
	s_barrier
; #define GAS __attribute__((address_space(1)))
; #define LAS __attribute__((address_space(3)))
; #define LDS_WAIT() asm volatile("s_waitcnt lgkmcnt(0)" ::: "memory")
; __device__ __forceinline__ unsigned pk4_fp8(float a, float b, float c, float d) {
;     a = fminf(fmaxf(a, -448.f), 448.f); b = fminf(fmaxf(b, -448.f), 448.f); c = fminf(fmaxf(c, -448.f), 448.f); d = fminf(fmaxf(d, -448.f), 448.f);
;     int w = __builtin_amdgcn_cvt_pk_fp8_f32(a, b, 0, false); w = __builtin_amdgcn_cvt_pk_fp8_f32(c, d, w, true); return (unsigned)w; }
;     const int pr = item >> 1, kb = 2 * (pr / nblk) + (item & 1), nb = pr % nblk, k0 = 64 * kb, n0 = 32 * nb;
;     const int nr = n0 + (lane & 31); const int sc = MAP == 1 ? src_col_in(nr) : nr;
;     float v[32];
; #pragma unroll
;     for (int i = 0; i < 32; ++i) v[i] = sc >= 0 ? W[(size_t)(k0 + 2 * i + (lane >> 5)) * Nsrc + sc] : 0.f;
; #pragma unroll
;     for (int i = 0; i < 32; ++i) { const int k = k0 + 2 * i + (lane >> 5); float x = v[i] * wscale; if (KS) x *= (k < ksplit ? ksA[k] : ksB[k - ksplit]); scr[(2 * i + (lane >> 5)) * 33 + (lane & 31)] = x; }
;     LDS_WAIT(); asm volatile("" ::: "memory");
;     const int c = lane & 7;
; #pragma unroll
;     for (int j = 0; j < 4; ++j) { const int n = (lane >> 3) + 8 * j; const LAS float* s = scr + (8 * c) * 33 + n;
;         const unsigned long long o = (unsigned long long)pg8::pk4_fp8(s[0 * 33], s[1 * 33], s[2 * 33], s[3 * 33]) | ((unsigned long long)pg8::pk4_fp8(s[4 * 33], s[5 * 33], s[6 * 33], s[7 * 33]) << 32);
;         *(GAS unsigned long long*)(WT + (size_t)(n0 + n) * K + k0 + 8 * c) = o; }
;     LDS_WAIT(); asm volatile("" ::: "memory");
	s_add_u32 s8, s30, 0xa000
	s_addc_u32 s9, s31, 0
	global_load_dwordx4 v[144:147], v74, s[8:9]
	s_add_u32 s8, s8, 0x20000
	s_addc_u32 s9, s9, 0
	global_load_dwordx4 v[148:151], v74, s[8:9]
	s_add_u32 s8, s8, 0x20000
	s_addc_u32 s9, s9, 0
	global_load_dwordx4 v[152:155], v74, s[8:9]
	s_add_u32 s8, s8, 0x20000
	s_addc_u32 s9, s9, 0
	global_load_dwordx4 v[156:159], v74, s[8:9]
	s_add_u32 s8, s8, 0x20000
	s_addc_u32 s9, s9, 0
	global_load_dwordx4 v[160:163], v74, s[8:9]
	s_add_u32 s8, s8, 0x20000
	s_addc_u32 s9, s9, 0
	global_load_dwordx4 v[164:167], v74, s[8:9]
	s_add_u32 s8, s8, 0x20000
	s_addc_u32 s9, s9, 0
	global_load_dwordx4 v[168:171], v74, s[8:9]
	s_add_u32 s8, s8, 0x20000
	s_addc_u32 s9, s9, 0
	global_load_dwordx4 v[172:175], v74, s[8:9]
	s_add_u32 s6, s32, 0x2000000
	s_addc_u32 s7, s33, 0
	ds_read_b32 v226, v211
	ds_read_b32 v227, v211 offset:512
	ds_read_b32 v228, v211 offset:1024
	ds_read_b32 v229, v211 offset:1536
	ds_read_b32 v230, v211 offset:2048
	ds_read_b32 v231, v211 offset:2560
	ds_read_b32 v232, v211 offset:3072
	ds_read_b32 v233, v211 offset:3584
	ds_read_b32 v234, v211 offset:4096
	ds_read_b32 v235, v211 offset:4608
	ds_read_b32 v236, v211 offset:5120
	ds_read_b32 v237, v211 offset:5632
	ds_read_b32 v238, v211 offset:6144
	ds_read_b32 v239, v211 offset:6656
	ds_read_b32 v240, v211 offset:7168
	ds_read_b32 v241, v211 offset:7680
	s_waitcnt lgkmcnt(0)
	v_max_f32_e32 v226, v226, v226
	v_max_f32_e32 v227, v227, v227
	v_max_f32_e32 v228, v228, v228
	v_max_f32_e32 v229, v229, v229
	v_max_f32_e32 v230, v230, v230
	v_max_f32_e32 v231, v231, v231
	v_max_f32_e32 v232, v232, v232
	v_max_f32_e32 v233, v233, v233
	v_max_f32_e32 v234, v234, v234
	v_max_f32_e32 v235, v235, v235
	v_max_f32_e32 v236, v236, v236
	v_max_f32_e32 v237, v237, v237
	v_max_f32_e32 v238, v238, v238
	v_max_f32_e32 v239, v239, v239
	v_max_f32_e32 v240, v240, v240
	v_max_f32_e32 v241, v241, v241
	v_med3_f32 v226, v226, s62, v95
	v_med3_f32 v227, v227, s62, v95
	v_med3_f32 v228, v228, s62, v95
	v_med3_f32 v229, v229, s62, v95
	v_med3_f32 v230, v230, s62, v95
	v_med3_f32 v231, v231, s62, v95
	v_med3_f32 v232, v232, s62, v95
	v_med3_f32 v233, v233, s62, v95
	v_med3_f32 v234, v234, s62, v95
	v_med3_f32 v235, v235, s62, v95
	v_med3_f32 v236, v236, s62, v95
	v_med3_f32 v237, v237, s62, v95
	v_med3_f32 v238, v238, s62, v95
	v_med3_f32 v239, v239, s62, v95
	v_med3_f32 v240, v240, s62, v95
	v_med3_f32 v241, v241, s62, v95
	v_mov_b32_e32 v242, 0
	v_mov_b32_e32 v243, 0
	v_mov_b32_e32 v244, 0
	v_mov_b32_e32 v245, 0
	v_cvt_pk_fp8_f32 v242, v226, v227
	v_cvt_pk_fp8_f32 v243, v230, v231
	v_cvt_pk_fp8_f32 v244, v234, v235
	v_cvt_pk_fp8_f32 v245, v238, v239
	v_cvt_pk_fp8_f32 v242, v228, v229 op_sel:[0,0,1]
	v_cvt_pk_fp8_f32 v243, v232, v233 op_sel:[0,0,1]
	v_cvt_pk_fp8_f32 v244, v236, v237 op_sel:[0,0,1]
	v_cvt_pk_fp8_f32 v245, v240, v241 op_sel:[0,0,1]
	s_nop 0
	global_store_dwordx4 v77, v[242:245], s[6:7]
	ds_read_b32 v226, v213
	ds_read_b32 v227, v213 offset:512
	ds_read_b32 v228, v213 offset:1024
	ds_read_b32 v229, v213 offset:1536
	ds_read_b32 v230, v213 offset:2048
	ds_read_b32 v231, v213 offset:2560
	ds_read_b32 v232, v213 offset:3072
	ds_read_b32 v233, v213 offset:3584
	ds_read_b32 v234, v213 offset:4096
	ds_read_b32 v235, v213 offset:4608
	ds_read_b32 v236, v213 offset:5120
	ds_read_b32 v237, v213 offset:5632
	ds_read_b32 v238, v213 offset:6144
	ds_read_b32 v239, v213 offset:6656
	ds_read_b32 v240, v213 offset:7168
	ds_read_b32 v241, v213 offset:7680
	s_waitcnt lgkmcnt(0)
	v_max_f32_e32 v226, v226, v226
	v_max_f32_e32 v227, v227, v227
	v_max_f32_e32 v228, v228, v228
	v_max_f32_e32 v229, v229, v229
	v_max_f32_e32 v230, v230, v230
	v_max_f32_e32 v231, v231, v231
	v_max_f32_e32 v232, v232, v232
	v_max_f32_e32 v233, v233, v233
	v_max_f32_e32 v234, v234, v234
	v_max_f32_e32 v235, v235, v235
	v_max_f32_e32 v236, v236, v236
	v_max_f32_e32 v237, v237, v237
	v_max_f32_e32 v238, v238, v238
	v_max_f32_e32 v239, v239, v239
	v_max_f32_e32 v240, v240, v240
	v_max_f32_e32 v241, v241, v241
	v_med3_f32 v226, v226, s62, v95
	v_med3_f32 v227, v227, s62, v95
	v_med3_f32 v228, v228, s62, v95
	v_med3_f32 v229, v229, s62, v95
	v_med3_f32 v230, v230, s62, v95
	v_med3_f32 v231, v231, s62, v95
	v_med3_f32 v232, v232, s62, v95
	v_med3_f32 v233, v233, s62, v95
	v_med3_f32 v234, v234, s62, v95
	v_med3_f32 v235, v235, s62, v95
	v_med3_f32 v236, v236, s62, v95
	v_med3_f32 v237, v237, s62, v95
	v_med3_f32 v238, v238, s62, v95
	v_med3_f32 v239, v239, s62, v95
	v_med3_f32 v240, v240, s62, v95
	v_med3_f32 v241, v241, s62, v95
	v_mov_b32_e32 v242, 0
	v_mov_b32_e32 v243, 0
	v_mov_b32_e32 v244, 0
	v_mov_b32_e32 v245, 0
	v_cvt_pk_fp8_f32 v242, v226, v227
	v_cvt_pk_fp8_f32 v243, v230, v231
	v_cvt_pk_fp8_f32 v244, v234, v235
	v_cvt_pk_fp8_f32 v245, v238, v239
	v_cvt_pk_fp8_f32 v242, v228, v229 op_sel:[0,0,1]
	v_cvt_pk_fp8_f32 v243, v232, v233 op_sel:[0,0,1]
	v_cvt_pk_fp8_f32 v244, v236, v237 op_sel:[0,0,1]
	v_cvt_pk_fp8_f32 v245, v240, v241 op_sel:[0,0,1]
	s_nop 0
	global_store_dwordx4 v78, v[242:245], s[6:7]
	s_waitcnt vmcnt(12)
	v_mul_f32_e32 v176, v26, v176
	v_mul_f32_e32 v177, v26, v177
	v_mul_f32_e32 v178, v26, v178
	v_mul_f32_e32 v179, v26, v179
	ds_write_b128 v210, v[176:179]
	v_mul_f32_e32 v180, v27, v180
	v_mul_f32_e32 v181, v27, v181
	v_mul_f32_e32 v182, v27, v182
	v_mul_f32_e32 v183, v27, v183
	ds_write_b128 v210, v[180:183] offset:1024
	v_mul_f32_e32 v184, v28, v184
	v_mul_f32_e32 v185, v28, v185
	v_mul_f32_e32 v186, v28, v186
	v_mul_f32_e32 v187, v28, v187
	ds_write_b128 v210, v[184:187] offset:2048
	v_mul_f32_e32 v188, v29, v188
	v_mul_f32_e32 v189, v29, v189
	v_mul_f32_e32 v190, v29, v190
	v_mul_f32_e32 v191, v29, v191
	ds_write_b128 v210, v[188:191] offset:3072
	v_mul_f32_e32 v192, v30, v192
	v_mul_f32_e32 v193, v30, v193
	v_mul_f32_e32 v194, v30, v194
	v_mul_f32_e32 v195, v30, v195
	ds_write_b128 v210, v[192:195] offset:4096
	v_mul_f32_e32 v196, v31, v196
	v_mul_f32_e32 v197, v31, v197
	v_mul_f32_e32 v198, v31, v198
	v_mul_f32_e32 v199, v31, v199
	ds_write_b128 v210, v[196:199] offset:5120
	v_mul_f32_e32 v200, v32, v200
	v_mul_f32_e32 v201, v32, v201
	v_mul_f32_e32 v202, v32, v202
	v_mul_f32_e32 v203, v32, v203
	ds_write_b128 v210, v[200:203] offset:6144
	v_mul_f32_e32 v204, v33, v204
	v_mul_f32_e32 v205, v33, v205
	v_mul_f32_e32 v206, v33, v206
	v_mul_f32_e32 v207, v33, v207
	ds_write_b128 v210, v[204:207] offset:7168
	s_waitcnt lgkmcnt(0)
	s_barrier
; #define GAS __attribute__((address_space(1)))
; #define LAS __attribute__((address_space(3)))
; #define LDS_WAIT() asm volatile("s_waitcnt lgkmcnt(0)" ::: "memory")
; __device__ __forceinline__ unsigned pk4_fp8(float a, float b, float c, float d) {
;     a = fminf(fmaxf(a, -448.f), 448.f); b = fminf(fmaxf(b, -448.f), 448.f); c = fminf(fmaxf(c, -448.f), 448.f); d = fminf(fmaxf(d, -448.f), 448.f);
;     int w = __builtin_amdgcn_cvt_pk_fp8_f32(a, b, 0, false); w = __builtin_amdgcn_cvt_pk_fp8_f32(c, d, w, true); return (unsigned)w; }
;     const int pr = item >> 1, kb = 2 * (pr / nblk) + (item & 1), nb = pr % nblk, k0 = 64 * kb, n0 = 32 * nb;
;     const int nr = n0 + (lane & 31); const int sc = MAP == 1 ? src_col_in(nr) : nr;
;     float v[32];
; #pragma unroll
;     for (int i = 0; i < 32; ++i) v[i] = sc >= 0 ? W[(size_t)(k0 + 2 * i + (lane >> 5)) * Nsrc + sc] : 0.f;
; #pragma unroll
;     for (int i = 0; i < 32; ++i) { const int k = k0 + 2 * i + (lane >> 5); float x = v[i] * wscale; if (KS) x *= (k < ksplit ? ksA[k] : ksB[k - ksplit]); scr[(2 * i + (lane >> 5)) * 33 + (lane & 31)] = x; }
;     LDS_WAIT(); asm volatile("" ::: "memory");
;     const int c = lane & 7;
; #pragma unroll
;     for (int j = 0; j < 4; ++j) { const int n = (lane >> 3) + 8 * j; const LAS float* s = scr + (8 * c) * 33 + n;
;         const unsigned long long o = (unsigned long long)pg8::pk4_fp8(s[0 * 33], s[1 * 33], s[2 * 33], s[3 * 33]) | ((unsigned long long)pg8::pk4_fp8(s[4 * 33], s[5 * 33], s[6 * 33], s[7 * 33]) << 32);
;         *(GAS unsigned long long*)(WT + (size_t)(n0 + n) * K + k0 + 8 * c) = o; }
;     LDS_WAIT(); asm volatile("" ::: "memory");
	s_add_u32 s8, s30, 0xb000
	s_addc_u32 s9, s31, 0
	global_load_dwordx4 v[176:179], v74, s[8:9]
	s_add_u32 s8, s8, 0x20000
	s_addc_u32 s9, s9, 0
	global_load_dwordx4 v[180:183], v74, s[8:9]
	s_add_u32 s8, s8, 0x20000
	s_addc_u32 s9, s9, 0
	global_load_dwordx4 v[184:187], v74, s[8:9]
	s_add_u32 s8, s8, 0x20000
	s_addc_u32 s9, s9, 0
	global_load_dwordx4 v[188:191], v74, s[8:9]
	s_add_u32 s8, s8, 0x20000
	s_addc_u32 s9, s9, 0
	global_load_dwordx4 v[192:195], v74, s[8:9]
	s_add_u32 s8, s8, 0x20000
	s_addc_u32 s9, s9, 0
	global_load_dwordx4 v[196:199], v74, s[8:9]
	s_add_u32 s8, s8, 0x20000
	s_addc_u32 s9, s9, 0
	global_load_dwordx4 v[200:203], v74, s[8:9]
	s_add_u32 s8, s8, 0x20000
	s_addc_u32 s9, s9, 0
	global_load_dwordx4 v[204:207], v74, s[8:9]
	s_add_u32 s6, s32, 0x2400000
	s_addc_u32 s7, s33, 0
	ds_read_b32 v226, v212
	ds_read_b32 v227, v212 offset:512
	ds_read_b32 v228, v212 offset:1024
	ds_read_b32 v229, v212 offset:1536
	ds_read_b32 v230, v212 offset:2048
	ds_read_b32 v231, v212 offset:2560
	ds_read_b32 v232, v212 offset:3072
	ds_read_b32 v233, v212 offset:3584
	ds_read_b32 v234, v212 offset:4096
	ds_read_b32 v235, v212 offset:4608
	ds_read_b32 v236, v212 offset:5120
	ds_read_b32 v237, v212 offset:5632
	ds_read_b32 v238, v212 offset:6144
	ds_read_b32 v239, v212 offset:6656
	ds_read_b32 v240, v212 offset:7168
	ds_read_b32 v241, v212 offset:7680
	s_waitcnt lgkmcnt(0)
	v_max_f32_e32 v226, v226, v226
	v_max_f32_e32 v227, v227, v227
	v_max_f32_e32 v228, v228, v228
	v_max_f32_e32 v229, v229, v229
	v_max_f32_e32 v230, v230, v230
	v_max_f32_e32 v231, v231, v231
	v_max_f32_e32 v232, v232, v232
	v_max_f32_e32 v233, v233, v233
	v_max_f32_e32 v234, v234, v234
	v_max_f32_e32 v235, v235, v235
	v_max_f32_e32 v236, v236, v236
	v_max_f32_e32 v237, v237, v237
	v_max_f32_e32 v238, v238, v238
	v_max_f32_e32 v239, v239, v239
	v_max_f32_e32 v240, v240, v240
	v_max_f32_e32 v241, v241, v241
	v_med3_f32 v226, v226, s62, v95
	v_med3_f32 v227, v227, s62, v95
	v_med3_f32 v228, v228, s62, v95
	v_med3_f32 v229, v229, s62, v95
	v_med3_f32 v230, v230, s62, v95
	v_med3_f32 v231, v231, s62, v95
	v_med3_f32 v232, v232, s62, v95
	v_med3_f32 v233, v233, s62, v95
	v_med3_f32 v234, v234, s62, v95
	v_med3_f32 v235, v235, s62, v95
	v_med3_f32 v236, v236, s62, v95
	v_med3_f32 v237, v237, s62, v95
	v_med3_f32 v238, v238, s62, v95
	v_med3_f32 v239, v239, s62, v95
	v_med3_f32 v240, v240, s62, v95
	v_med3_f32 v241, v241, s62, v95
	v_mov_b32_e32 v242, 0
	v_mov_b32_e32 v243, 0
	v_mov_b32_e32 v244, 0
	v_mov_b32_e32 v245, 0
	v_cvt_pk_fp8_f32 v242, v226, v227
	v_cvt_pk_fp8_f32 v243, v230, v231
	v_cvt_pk_fp8_f32 v244, v234, v235
	v_cvt_pk_fp8_f32 v245, v238, v239
	v_cvt_pk_fp8_f32 v242, v228, v229 op_sel:[0,0,1]
	v_cvt_pk_fp8_f32 v243, v232, v233 op_sel:[0,0,1]
	v_cvt_pk_fp8_f32 v244, v236, v237 op_sel:[0,0,1]
	v_cvt_pk_fp8_f32 v245, v240, v241 op_sel:[0,0,1]
	s_nop 0
	global_store_dwordx4 v77, v[242:245], s[6:7]
	ds_read_b32 v226, v214
	ds_read_b32 v227, v214 offset:512
	ds_read_b32 v228, v214 offset:1024
	ds_read_b32 v229, v214 offset:1536
	ds_read_b32 v230, v214 offset:2048
	ds_read_b32 v231, v214 offset:2560
	ds_read_b32 v232, v214 offset:3072
	ds_read_b32 v233, v214 offset:3584
	ds_read_b32 v234, v214 offset:4096
	ds_read_b32 v235, v214 offset:4608
	ds_read_b32 v236, v214 offset:5120
	ds_read_b32 v237, v214 offset:5632
	ds_read_b32 v238, v214 offset:6144
	ds_read_b32 v239, v214 offset:6656
	ds_read_b32 v240, v214 offset:7168
	ds_read_b32 v241, v214 offset:7680
	s_waitcnt lgkmcnt(0)
	v_max_f32_e32 v226, v226, v226
	v_max_f32_e32 v227, v227, v227
	v_max_f32_e32 v228, v228, v228
	v_max_f32_e32 v229, v229, v229
	v_max_f32_e32 v230, v230, v230
	v_max_f32_e32 v231, v231, v231
	v_max_f32_e32 v232, v232, v232
	v_max_f32_e32 v233, v233, v233
	v_max_f32_e32 v234, v234, v234
	v_max_f32_e32 v235, v235, v235
	v_max_f32_e32 v236, v236, v236
	v_max_f32_e32 v237, v237, v237
	v_max_f32_e32 v238, v238, v238
	v_max_f32_e32 v239, v239, v239
	v_max_f32_e32 v240, v240, v240
	v_max_f32_e32 v241, v241, v241
	v_med3_f32 v226, v226, s62, v95
	v_med3_f32 v227, v227, s62, v95
	v_med3_f32 v228, v228, s62, v95
	v_med3_f32 v229, v229, s62, v95
	v_med3_f32 v230, v230, s62, v95
	v_med3_f32 v231, v231, s62, v95
	v_med3_f32 v232, v232, s62, v95
	v_med3_f32 v233, v233, s62, v95
	v_med3_f32 v234, v234, s62, v95
	v_med3_f32 v235, v235, s62, v95
	v_med3_f32 v236, v236, s62, v95
	v_med3_f32 v237, v237, s62, v95
	v_med3_f32 v238, v238, s62, v95
	v_med3_f32 v239, v239, s62, v95
	v_med3_f32 v240, v240, s62, v95
	v_med3_f32 v241, v241, s62, v95
	v_mov_b32_e32 v242, 0
	v_mov_b32_e32 v243, 0
	v_mov_b32_e32 v244, 0
	v_mov_b32_e32 v245, 0
	v_cvt_pk_fp8_f32 v242, v226, v227
	v_cvt_pk_fp8_f32 v243, v230, v231
	v_cvt_pk_fp8_f32 v244, v234, v235
	v_cvt_pk_fp8_f32 v245, v238, v239
	v_cvt_pk_fp8_f32 v242, v228, v229 op_sel:[0,0,1]
	v_cvt_pk_fp8_f32 v243, v232, v233 op_sel:[0,0,1]
	v_cvt_pk_fp8_f32 v244, v236, v237 op_sel:[0,0,1]
	v_cvt_pk_fp8_f32 v245, v240, v241 op_sel:[0,0,1]
	s_nop 0
	global_store_dwordx4 v78, v[242:245], s[6:7]
	s_waitcnt vmcnt(12)
	v_mul_f32_e32 v144, v26, v144
	v_mul_f32_e32 v145, v26, v145
	v_mul_f32_e32 v146, v26, v146
	v_mul_f32_e32 v147, v26, v147
	ds_write_b128 v209, v[144:147]
	v_mul_f32_e32 v148, v27, v148
	v_mul_f32_e32 v149, v27, v149
	v_mul_f32_e32 v150, v27, v150
	v_mul_f32_e32 v151, v27, v151
	ds_write_b128 v209, v[148:151] offset:1024
	v_mul_f32_e32 v152, v28, v152
	v_mul_f32_e32 v153, v28, v153
	v_mul_f32_e32 v154, v28, v154
	v_mul_f32_e32 v155, v28, v155
	ds_write_b128 v209, v[152:155] offset:2048
	v_mul_f32_e32 v156, v29, v156
	v_mul_f32_e32 v157, v29, v157
	v_mul_f32_e32 v158, v29, v158
	v_mul_f32_e32 v159, v29, v159
	ds_write_b128 v209, v[156:159] offset:3072
	v_mul_f32_e32 v160, v30, v160
	v_mul_f32_e32 v161, v30, v161
	v_mul_f32_e32 v162, v30, v162
	v_mul_f32_e32 v163, v30, v163
	ds_write_b128 v209, v[160:163] offset:4096
	v_mul_f32_e32 v164, v31, v164
	v_mul_f32_e32 v165, v31, v165
	v_mul_f32_e32 v166, v31, v166
	v_mul_f32_e32 v167, v31, v167
	ds_write_b128 v209, v[164:167] offset:5120
	v_mul_f32_e32 v168, v32, v168
	v_mul_f32_e32 v169, v32, v169
	v_mul_f32_e32 v170, v32, v170
	v_mul_f32_e32 v171, v32, v171
	ds_write_b128 v209, v[168:171] offset:6144
	v_mul_f32_e32 v172, v33, v172
	v_mul_f32_e32 v173, v33, v173
	v_mul_f32_e32 v174, v33, v174
	v_mul_f32_e32 v175, v33, v175
	ds_write_b128 v209, v[172:175] offset:7168
	s_waitcnt lgkmcnt(0)
	s_barrier
; #define GAS __attribute__((address_space(1)))
; #define LAS __attribute__((address_space(3)))
; #define LDS_WAIT() asm volatile("s_waitcnt lgkmcnt(0)" ::: "memory")
; __device__ __forceinline__ unsigned pk4_fp8(float a, float b, float c, float d) {
;     a = fminf(fmaxf(a, -448.f), 448.f); b = fminf(fmaxf(b, -448.f), 448.f); c = fminf(fmaxf(c, -448.f), 448.f); d = fminf(fmaxf(d, -448.f), 448.f);
;     int w = __builtin_amdgcn_cvt_pk_fp8_f32(a, b, 0, false); w = __builtin_amdgcn_cvt_pk_fp8_f32(c, d, w, true); return (unsigned)w; }
;     const int pr = item >> 1, kb = 2 * (pr / nblk) + (item & 1), nb = pr % nblk, k0 = 64 * kb, n0 = 32 * nb;
;     const int nr = n0 + (lane & 31); const int sc = MAP == 1 ? src_col_in(nr) : nr;
;     float v[32];
; #pragma unroll
;     for (int i = 0; i < 32; ++i) v[i] = sc >= 0 ? W[(size_t)(k0 + 2 * i + (lane >> 5)) * Nsrc + sc] : 0.f;
; #pragma unroll
;     for (int i = 0; i < 32; ++i) { const int k = k0 + 2 * i + (lane >> 5); float x = v[i] * wscale; if (KS) x *= (k < ksplit ? ksA[k] : ksB[k - ksplit]); scr[(2 * i + (lane >> 5)) * 33 + (lane & 31)] = x; }
;     LDS_WAIT(); asm volatile("" ::: "memory");
;     const int c = lane & 7;
; #pragma unroll
;     for (int j = 0; j < 4; ++j) { const int n = (lane >> 3) + 8 * j; const LAS float* s = scr + (8 * c) * 33 + n;
;         const unsigned long long o = (unsigned long long)pg8::pk4_fp8(s[0 * 33], s[1 * 33], s[2 * 33], s[3 * 33]) | ((unsigned long long)pg8::pk4_fp8(s[4 * 33], s[5 * 33], s[6 * 33], s[7 * 33]) << 32);
;         *(GAS unsigned long long*)(WT + (size_t)(n0 + n) * K + k0 + 8 * c) = o; }
;     LDS_WAIT(); asm volatile("" ::: "memory");
	s_add_u32 s8, s30, 0xc000
	s_addc_u32 s9, s31, 0
	global_load_dwordx4 v[144:147], v74, s[8:9]
	s_add_u32 s8, s8, 0x20000
	s_addc_u32 s9, s9, 0
	global_load_dwordx4 v[148:151], v74, s[8:9]
	s_add_u32 s8, s8, 0x20000
	s_addc_u32 s9, s9, 0
	global_load_dwordx4 v[152:155], v74, s[8:9]
	s_add_u32 s8, s8, 0x20000
	s_addc_u32 s9, s9, 0
	global_load_dwordx4 v[156:159], v74, s[8:9]
	s_add_u32 s8, s8, 0x20000
	s_addc_u32 s9, s9, 0
	global_load_dwordx4 v[160:163], v74, s[8:9]
	s_add_u32 s8, s8, 0x20000
	s_addc_u32 s9, s9, 0
	global_load_dwordx4 v[164:167], v74, s[8:9]
	s_add_u32 s8, s8, 0x20000
	s_addc_u32 s9, s9, 0
	global_load_dwordx4 v[168:171], v74, s[8:9]
	s_add_u32 s8, s8, 0x20000
	s_addc_u32 s9, s9, 0
	global_load_dwordx4 v[172:175], v74, s[8:9]
	s_add_u32 s6, s32, 0x2800000
	s_addc_u32 s7, s33, 0
	ds_read_b32 v226, v211
	ds_read_b32 v227, v211 offset:512
	ds_read_b32 v228, v211 offset:1024
	ds_read_b32 v229, v211 offset:1536
	ds_read_b32 v230, v211 offset:2048
	ds_read_b32 v231, v211 offset:2560
	ds_read_b32 v232, v211 offset:3072
	ds_read_b32 v233, v211 offset:3584
	ds_read_b32 v234, v211 offset:4096
	ds_read_b32 v235, v211 offset:4608
	ds_read_b32 v236, v211 offset:5120
	ds_read_b32 v237, v211 offset:5632
	ds_read_b32 v238, v211 offset:6144
	ds_read_b32 v239, v211 offset:6656
	ds_read_b32 v240, v211 offset:7168
	ds_read_b32 v241, v211 offset:7680
	s_waitcnt lgkmcnt(0)
	v_max_f32_e32 v226, v226, v226
	v_max_f32_e32 v227, v227, v227
	v_max_f32_e32 v228, v228, v228
	v_max_f32_e32 v229, v229, v229
	v_max_f32_e32 v230, v230, v230
	v_max_f32_e32 v231, v231, v231
	v_max_f32_e32 v232, v232, v232
	v_max_f32_e32 v233, v233, v233
	v_max_f32_e32 v234, v234, v234
	v_max_f32_e32 v235, v235, v235
	v_max_f32_e32 v236, v236, v236
	v_max_f32_e32 v237, v237, v237
	v_max_f32_e32 v238, v238, v238
	v_max_f32_e32 v239, v239, v239
	v_max_f32_e32 v240, v240, v240
	v_max_f32_e32 v241, v241, v241
	v_med3_f32 v226, v226, s62, v95
	v_med3_f32 v227, v227, s62, v95
	v_med3_f32 v228, v228, s62, v95
	v_med3_f32 v229, v229, s62, v95
	v_med3_f32 v230, v230, s62, v95
	v_med3_f32 v231, v231, s62, v95
	v_med3_f32 v232, v232, s62, v95
	v_med3_f32 v233, v233, s62, v95
	v_med3_f32 v234, v234, s62, v95
	v_med3_f32 v235, v235, s62, v95
	v_med3_f32 v236, v236, s62, v95
	v_med3_f32 v237, v237, s62, v95
	v_med3_f32 v238, v238, s62, v95
	v_med3_f32 v239, v239, s62, v95
	v_med3_f32 v240, v240, s62, v95
	v_med3_f32 v241, v241, s62, v95
	v_mov_b32_e32 v242, 0
	v_mov_b32_e32 v243, 0
	v_mov_b32_e32 v244, 0
	v_mov_b32_e32 v245, 0
	v_cvt_pk_fp8_f32 v242, v226, v227
	v_cvt_pk_fp8_f32 v243, v230, v231
	v_cvt_pk_fp8_f32 v244, v234, v235
	v_cvt_pk_fp8_f32 v245, v238, v239
	v_cvt_pk_fp8_f32 v242, v228, v229 op_sel:[0,0,1]
	v_cvt_pk_fp8_f32 v243, v232, v233 op_sel:[0,0,1]
	v_cvt_pk_fp8_f32 v244, v236, v237 op_sel:[0,0,1]
	v_cvt_pk_fp8_f32 v245, v240, v241 op_sel:[0,0,1]
	s_nop 0
	global_store_dwordx4 v77, v[242:245], s[6:7]
	ds_read_b32 v226, v213
	ds_read_b32 v227, v213 offset:512
	ds_read_b32 v228, v213 offset:1024
	ds_read_b32 v229, v213 offset:1536
	ds_read_b32 v230, v213 offset:2048
	ds_read_b32 v231, v213 offset:2560
	ds_read_b32 v232, v213 offset:3072
	ds_read_b32 v233, v213 offset:3584
	ds_read_b32 v234, v213 offset:4096
	ds_read_b32 v235, v213 offset:4608
	ds_read_b32 v236, v213 offset:5120
	ds_read_b32 v237, v213 offset:5632
	ds_read_b32 v238, v213 offset:6144
	ds_read_b32 v239, v213 offset:6656
	ds_read_b32 v240, v213 offset:7168
	ds_read_b32 v241, v213 offset:7680
	s_waitcnt lgkmcnt(0)
	v_max_f32_e32 v226, v226, v226
	v_max_f32_e32 v227, v227, v227
	v_max_f32_e32 v228, v228, v228
	v_max_f32_e32 v229, v229, v229
	v_max_f32_e32 v230, v230, v230
	v_max_f32_e32 v231, v231, v231
	v_max_f32_e32 v232, v232, v232
	v_max_f32_e32 v233, v233, v233
	v_max_f32_e32 v234, v234, v234
	v_max_f32_e32 v235, v235, v235
	v_max_f32_e32 v236, v236, v236
	v_max_f32_e32 v237, v237, v237
	v_max_f32_e32 v238, v238, v238
	v_max_f32_e32 v239, v239, v239
	v_max_f32_e32 v240, v240, v240
	v_max_f32_e32 v241, v241, v241
	v_med3_f32 v226, v226, s62, v95
	v_med3_f32 v227, v227, s62, v95
	v_med3_f32 v228, v228, s62, v95
	v_med3_f32 v229, v229, s62, v95
	v_med3_f32 v230, v230, s62, v95
	v_med3_f32 v231, v231, s62, v95
	v_med3_f32 v232, v232, s62, v95
	v_med3_f32 v233, v233, s62, v95
	v_med3_f32 v234, v234, s62, v95
	v_med3_f32 v235, v235, s62, v95
	v_med3_f32 v236, v236, s62, v95
	v_med3_f32 v237, v237, s62, v95
	v_med3_f32 v238, v238, s62, v95
	v_med3_f32 v239, v239, s62, v95
	v_med3_f32 v240, v240, s62, v95
	v_med3_f32 v241, v241, s62, v95
	v_mov_b32_e32 v242, 0
	v_mov_b32_e32 v243, 0
	v_mov_b32_e32 v244, 0
	v_mov_b32_e32 v245, 0
	v_cvt_pk_fp8_f32 v242, v226, v227
	v_cvt_pk_fp8_f32 v243, v230, v231
	v_cvt_pk_fp8_f32 v244, v234, v235
	v_cvt_pk_fp8_f32 v245, v238, v239
	v_cvt_pk_fp8_f32 v242, v228, v229 op_sel:[0,0,1]
	v_cvt_pk_fp8_f32 v243, v232, v233 op_sel:[0,0,1]
	v_cvt_pk_fp8_f32 v244, v236, v237 op_sel:[0,0,1]
	v_cvt_pk_fp8_f32 v245, v240, v241 op_sel:[0,0,1]
	s_nop 0
	global_store_dwordx4 v78, v[242:245], s[6:7]
	s_waitcnt vmcnt(12)
	v_mul_f32_e32 v176, v26, v176
	v_mul_f32_e32 v177, v26, v177
	v_mul_f32_e32 v178, v26, v178
	v_mul_f32_e32 v179, v26, v179
	ds_write_b128 v210, v[176:179]
	v_mul_f32_e32 v180, v27, v180
	v_mul_f32_e32 v181, v27, v181
	v_mul_f32_e32 v182, v27, v182
	v_mul_f32_e32 v183, v27, v183
	ds_write_b128 v210, v[180:183] offset:1024
	v_mul_f32_e32 v184, v28, v184
	v_mul_f32_e32 v185, v28, v185
	v_mul_f32_e32 v186, v28, v186
	v_mul_f32_e32 v187, v28, v187
	ds_write_b128 v210, v[184:187] offset:2048
	v_mul_f32_e32 v188, v29, v188
	v_mul_f32_e32 v189, v29, v189
	v_mul_f32_e32 v190, v29, v190
	v_mul_f32_e32 v191, v29, v191
	ds_write_b128 v210, v[188:191] offset:3072
	v_mul_f32_e32 v192, v30, v192
	v_mul_f32_e32 v193, v30, v193
	v_mul_f32_e32 v194, v30, v194
	v_mul_f32_e32 v195, v30, v195
	ds_write_b128 v210, v[192:195] offset:4096
	v_mul_f32_e32 v196, v31, v196
	v_mul_f32_e32 v197, v31, v197
	v_mul_f32_e32 v198, v31, v198
	v_mul_f32_e32 v199, v31, v199
	ds_write_b128 v210, v[196:199] offset:5120
	v_mul_f32_e32 v200, v32, v200
	v_mul_f32_e32 v201, v32, v201
	v_mul_f32_e32 v202, v32, v202
	v_mul_f32_e32 v203, v32, v203
	ds_write_b128 v210, v[200:203] offset:6144
	v_mul_f32_e32 v204, v33, v204
	v_mul_f32_e32 v205, v33, v205
	v_mul_f32_e32 v206, v33, v206
	v_mul_f32_e32 v207, v33, v207
	ds_write_b128 v210, v[204:207] offset:7168
	s_waitcnt lgkmcnt(0)
	s_barrier
; #define GAS __attribute__((address_space(1)))
; #define LAS __attribute__((address_space(3)))
; #define LDS_WAIT() asm volatile("s_waitcnt lgkmcnt(0)" ::: "memory")
; __device__ __forceinline__ unsigned pk4_fp8(float a, float b, float c, float d) {
;     a = fminf(fmaxf(a, -448.f), 448.f); b = fminf(fmaxf(b, -448.f), 448.f); c = fminf(fmaxf(c, -448.f), 448.f); d = fminf(fmaxf(d, -448.f), 448.f);
;     int w = __builtin_amdgcn_cvt_pk_fp8_f32(a, b, 0, false); w = __builtin_amdgcn_cvt_pk_fp8_f32(c, d, w, true); return (unsigned)w; }
;     const int pr = item >> 1, kb = 2 * (pr / nblk) + (item & 1), nb = pr % nblk, k0 = 64 * kb, n0 = 32 * nb;
;     const int nr = n0 + (lane & 31); const int sc = MAP == 1 ? src_col_in(nr) : nr;
;     float v[32];
; #pragma unroll
;     for (int i = 0; i < 32; ++i) v[i] = sc >= 0 ? W[(size_t)(k0 + 2 * i + (lane >> 5)) * Nsrc + sc] : 0.f;
; #pragma unroll
;     for (int i = 0; i < 32; ++i) { const int k = k0 + 2 * i + (lane >> 5); float x = v[i] * wscale; if (KS) x *= (k < ksplit ? ksA[k] : ksB[k - ksplit]); scr[(2 * i + (lane >> 5)) * 33 + (lane & 31)] = x; }
;     LDS_WAIT(); asm volatile("" ::: "memory");
;     const int c = lane & 7;
; #pragma unroll
;     for (int j = 0; j < 4; ++j) { const int n = (lane >> 3) + 8 * j; const LAS float* s = scr + (8 * c) * 33 + n;
;         const unsigned long long o = (unsigned long long)pg8::pk4_fp8(s[0 * 33], s[1 * 33], s[2 * 33], s[3 * 33]) | ((unsigned long long)pg8::pk4_fp8(s[4 * 33], s[5 * 33], s[6 * 33], s[7 * 33]) << 32);
;         *(GAS unsigned long long*)(WT + (size_t)(n0 + n) * K + k0 + 8 * c) = o; }
;     LDS_WAIT(); asm volatile("" ::: "memory");
	s_add_u32 s8, s30, 0xd000
	s_addc_u32 s9, s31, 0
	global_load_dwordx4 v[176:179], v74, s[8:9]
	s_add_u32 s8, s8, 0x20000
	s_addc_u32 s9, s9, 0
	global_load_dwordx4 v[180:183], v74, s[8:9]
	s_add_u32 s8, s8, 0x20000
	s_addc_u32 s9, s9, 0
	global_load_dwordx4 v[184:187], v74, s[8:9]
	s_add_u32 s8, s8, 0x20000
	s_addc_u32 s9, s9, 0
	global_load_dwordx4 v[188:191], v74, s[8:9]
	s_add_u32 s8, s8, 0x20000
	s_addc_u32 s9, s9, 0
	global_load_dwordx4 v[192:195], v74, s[8:9]
	s_add_u32 s8, s8, 0x20000
	s_addc_u32 s9, s9, 0
	global_load_dwordx4 v[196:199], v74, s[8:9]
	s_add_u32 s8, s8, 0x20000
	s_addc_u32 s9, s9, 0
	global_load_dwordx4 v[200:203], v74, s[8:9]
	s_add_u32 s8, s8, 0x20000
	s_addc_u32 s9, s9, 0
	global_load_dwordx4 v[204:207], v74, s[8:9]
	s_add_u32 s6, s32, 0x2c00000
	s_addc_u32 s7, s33, 0
	ds_read_b32 v226, v212
	ds_read_b32 v227, v212 offset:512
	ds_read_b32 v228, v212 offset:1024
	ds_read_b32 v229, v212 offset:1536
	ds_read_b32 v230, v212 offset:2048
	ds_read_b32 v231, v212 offset:2560
	ds_read_b32 v232, v212 offset:3072
	ds_read_b32 v233, v212 offset:3584
	ds_read_b32 v234, v212 offset:4096
	ds_read_b32 v235, v212 offset:4608
	ds_read_b32 v236, v212 offset:5120
	ds_read_b32 v237, v212 offset:5632
	ds_read_b32 v238, v212 offset:6144
	ds_read_b32 v239, v212 offset:6656
	ds_read_b32 v240, v212 offset:7168
	ds_read_b32 v241, v212 offset:7680
	s_waitcnt lgkmcnt(0)
	v_max_f32_e32 v226, v226, v226
	v_max_f32_e32 v227, v227, v227
	v_max_f32_e32 v228, v228, v228
	v_max_f32_e32 v229, v229, v229
	v_max_f32_e32 v230, v230, v230
	v_max_f32_e32 v231, v231, v231
	v_max_f32_e32 v232, v232, v232
	v_max_f32_e32 v233, v233, v233
	v_max_f32_e32 v234, v234, v234
	v_max_f32_e32 v235, v235, v235
	v_max_f32_e32 v236, v236, v236
	v_max_f32_e32 v237, v237, v237
	v_max_f32_e32 v238, v238, v238
	v_max_f32_e32 v239, v239, v239
	v_max_f32_e32 v240, v240, v240
	v_max_f32_e32 v241, v241, v241
	v_med3_f32 v226, v226, s62, v95
	v_med3_f32 v227, v227, s62, v95
	v_med3_f32 v228, v228, s62, v95
	v_med3_f32 v229, v229, s62, v95
	v_med3_f32 v230, v230, s62, v95
	v_med3_f32 v231, v231, s62, v95
	v_med3_f32 v232, v232, s62, v95
	v_med3_f32 v233, v233, s62, v95
	v_med3_f32 v234, v234, s62, v95
	v_med3_f32 v235, v235, s62, v95
	v_med3_f32 v236, v236, s62, v95
	v_med3_f32 v237, v237, s62, v95
	v_med3_f32 v238, v238, s62, v95
	v_med3_f32 v239, v239, s62, v95
	v_med3_f32 v240, v240, s62, v95
	v_med3_f32 v241, v241, s62, v95
	v_mov_b32_e32 v242, 0
	v_mov_b32_e32 v243, 0
	v_mov_b32_e32 v244, 0
	v_mov_b32_e32 v245, 0
	v_cvt_pk_fp8_f32 v242, v226, v227
	v_cvt_pk_fp8_f32 v243, v230, v231
	v_cvt_pk_fp8_f32 v244, v234, v235
	v_cvt_pk_fp8_f32 v245, v238, v239
	v_cvt_pk_fp8_f32 v242, v228, v229 op_sel:[0,0,1]
	v_cvt_pk_fp8_f32 v243, v232, v233 op_sel:[0,0,1]
	v_cvt_pk_fp8_f32 v244, v236, v237 op_sel:[0,0,1]
	v_cvt_pk_fp8_f32 v245, v240, v241 op_sel:[0,0,1]
	s_nop 0
	global_store_dwordx4 v77, v[242:245], s[6:7]
	ds_read_b32 v226, v214
	ds_read_b32 v227, v214 offset:512
	ds_read_b32 v228, v214 offset:1024
	ds_read_b32 v229, v214 offset:1536
	ds_read_b32 v230, v214 offset:2048
	ds_read_b32 v231, v214 offset:2560
	ds_read_b32 v232, v214 offset:3072
	ds_read_b32 v233, v214 offset:3584
	ds_read_b32 v234, v214 offset:4096
	ds_read_b32 v235, v214 offset:4608
	ds_read_b32 v236, v214 offset:5120
	ds_read_b32 v237, v214 offset:5632
	ds_read_b32 v238, v214 offset:6144
	ds_read_b32 v239, v214 offset:6656
	ds_read_b32 v240, v214 offset:7168
	ds_read_b32 v241, v214 offset:7680
	s_waitcnt lgkmcnt(0)
	v_max_f32_e32 v226, v226, v226
	v_max_f32_e32 v227, v227, v227
	v_max_f32_e32 v228, v228, v228
	v_max_f32_e32 v229, v229, v229
	v_max_f32_e32 v230, v230, v230
	v_max_f32_e32 v231, v231, v231
	v_max_f32_e32 v232, v232, v232
	v_max_f32_e32 v233, v233, v233
	v_max_f32_e32 v234, v234, v234
	v_max_f32_e32 v235, v235, v235
	v_max_f32_e32 v236, v236, v236
	v_max_f32_e32 v237, v237, v237
	v_max_f32_e32 v238, v238, v238
	v_max_f32_e32 v239, v239, v239
	v_max_f32_e32 v240, v240, v240
	v_max_f32_e32 v241, v241, v241
	v_med3_f32 v226, v226, s62, v95
	v_med3_f32 v227, v227, s62, v95
	v_med3_f32 v228, v228, s62, v95
	v_med3_f32 v229, v229, s62, v95
	v_med3_f32 v230, v230, s62, v95
	v_med3_f32 v231, v231, s62, v95
	v_med3_f32 v232, v232, s62, v95
	v_med3_f32 v233, v233, s62, v95
	v_med3_f32 v234, v234, s62, v95
	v_med3_f32 v235, v235, s62, v95
	v_med3_f32 v236, v236, s62, v95
	v_med3_f32 v237, v237, s62, v95
	v_med3_f32 v238, v238, s62, v95
	v_med3_f32 v239, v239, s62, v95
	v_med3_f32 v240, v240, s62, v95
	v_med3_f32 v241, v241, s62, v95
	v_mov_b32_e32 v242, 0
	v_mov_b32_e32 v243, 0
	v_mov_b32_e32 v244, 0
	v_mov_b32_e32 v245, 0
	v_cvt_pk_fp8_f32 v242, v226, v227
	v_cvt_pk_fp8_f32 v243, v230, v231
	v_cvt_pk_fp8_f32 v244, v234, v235
	v_cvt_pk_fp8_f32 v245, v238, v239
	v_cvt_pk_fp8_f32 v242, v228, v229 op_sel:[0,0,1]
	v_cvt_pk_fp8_f32 v243, v232, v233 op_sel:[0,0,1]
	v_cvt_pk_fp8_f32 v244, v236, v237 op_sel:[0,0,1]
	v_cvt_pk_fp8_f32 v245, v240, v241 op_sel:[0,0,1]
	s_nop 0
	global_store_dwordx4 v78, v[242:245], s[6:7]
	s_waitcnt vmcnt(12)
	v_mul_f32_e32 v144, v26, v144
	v_mul_f32_e32 v145, v26, v145
	v_mul_f32_e32 v146, v26, v146
	v_mul_f32_e32 v147, v26, v147
	ds_write_b128 v209, v[144:147]
	v_mul_f32_e32 v148, v27, v148
	v_mul_f32_e32 v149, v27, v149
	v_mul_f32_e32 v150, v27, v150
	v_mul_f32_e32 v151, v27, v151
	ds_write_b128 v209, v[148:151] offset:1024
	v_mul_f32_e32 v152, v28, v152
	v_mul_f32_e32 v153, v28, v153
	v_mul_f32_e32 v154, v28, v154
	v_mul_f32_e32 v155, v28, v155
	ds_write_b128 v209, v[152:155] offset:2048
	v_mul_f32_e32 v156, v29, v156
	v_mul_f32_e32 v157, v29, v157
	v_mul_f32_e32 v158, v29, v158
	v_mul_f32_e32 v159, v29, v159
	ds_write_b128 v209, v[156:159] offset:3072
	v_mul_f32_e32 v160, v30, v160
	v_mul_f32_e32 v161, v30, v161
	v_mul_f32_e32 v162, v30, v162
	v_mul_f32_e32 v163, v30, v163
	ds_write_b128 v209, v[160:163] offset:4096
	v_mul_f32_e32 v164, v31, v164
	v_mul_f32_e32 v165, v31, v165
	v_mul_f32_e32 v166, v31, v166
	v_mul_f32_e32 v167, v31, v167
	ds_write_b128 v209, v[164:167] offset:5120
	v_mul_f32_e32 v168, v32, v168
	v_mul_f32_e32 v169, v32, v169
	v_mul_f32_e32 v170, v32, v170
	v_mul_f32_e32 v171, v32, v171
	ds_write_b128 v209, v[168:171] offset:6144
	v_mul_f32_e32 v172, v33, v172
	v_mul_f32_e32 v173, v33, v173
	v_mul_f32_e32 v174, v33, v174
	v_mul_f32_e32 v175, v33, v175
	ds_write_b128 v209, v[172:175] offset:7168
	s_waitcnt lgkmcnt(0)
	s_barrier
; #define GAS __attribute__((address_space(1)))
; #define LAS __attribute__((address_space(3)))
; #define LDS_WAIT() asm volatile("s_waitcnt lgkmcnt(0)" ::: "memory")
; __device__ __forceinline__ unsigned pk4_fp8(float a, float b, float c, float d) {
;     a = fminf(fmaxf(a, -448.f), 448.f); b = fminf(fmaxf(b, -448.f), 448.f); c = fminf(fmaxf(c, -448.f), 448.f); d = fminf(fmaxf(d, -448.f), 448.f);
;     int w = __builtin_amdgcn_cvt_pk_fp8_f32(a, b, 0, false); w = __builtin_amdgcn_cvt_pk_fp8_f32(c, d, w, true); return (unsigned)w; }
;     const int pr = item >> 1, kb = 2 * (pr / nblk) + (item & 1), nb = pr % nblk, k0 = 64 * kb, n0 = 32 * nb;
;     const int nr = n0 + (lane & 31); const int sc = MAP == 1 ? src_col_in(nr) : nr;
;     float v[32];
; #pragma unroll
;     for (int i = 0; i < 32; ++i) v[i] = sc >= 0 ? W[(size_t)(k0 + 2 * i + (lane >> 5)) * Nsrc + sc] : 0.f;
; #pragma unroll
;     for (int i = 0; i < 32; ++i) { const int k = k0 + 2 * i + (lane >> 5); float x = v[i] * wscale; if (KS) x *= (k < ksplit ? ksA[k] : ksB[k - ksplit]); scr[(2 * i + (lane >> 5)) * 33 + (lane & 31)] = x; }
;     LDS_WAIT(); asm volatile("" ::: "memory");
;     const int c = lane & 7;
; #pragma unroll
;     for (int j = 0; j < 4; ++j) { const int n = (lane >> 3) + 8 * j; const LAS float* s = scr + (8 * c) * 33 + n;
;         const unsigned long long o = (unsigned long long)pg8::pk4_fp8(s[0 * 33], s[1 * 33], s[2 * 33], s[3 * 33]) | ((unsigned long long)pg8::pk4_fp8(s[4 * 33], s[5 * 33], s[6 * 33], s[7 * 33]) << 32);
;         *(GAS unsigned long long*)(WT + (size_t)(n0 + n) * K + k0 + 8 * c) = o; }
;     LDS_WAIT(); asm volatile("" ::: "memory");
	s_add_u32 s8, s30, 0xe000
	s_addc_u32 s9, s31, 0
	global_load_dwordx4 v[144:147], v74, s[8:9]
	s_add_u32 s8, s8, 0x20000
	s_addc_u32 s9, s9, 0
	global_load_dwordx4 v[148:151], v74, s[8:9]
	s_add_u32 s8, s8, 0x20000
	s_addc_u32 s9, s9, 0
	global_load_dwordx4 v[152:155], v74, s[8:9]
	s_add_u32 s8, s8, 0x20000
	s_addc_u32 s9, s9, 0
	global_load_dwordx4 v[156:159], v74, s[8:9]
	s_add_u32 s8, s8, 0x20000
	s_addc_u32 s9, s9, 0
	global_load_dwordx4 v[160:163], v74, s[8:9]
	s_add_u32 s8, s8, 0x20000
	s_addc_u32 s9, s9, 0
	global_load_dwordx4 v[164:167], v74, s[8:9]
	s_add_u32 s8, s8, 0x20000
	s_addc_u32 s9, s9, 0
	global_load_dwordx4 v[168:171], v74, s[8:9]
	s_add_u32 s8, s8, 0x20000
	s_addc_u32 s9, s9, 0
	global_load_dwordx4 v[172:175], v74, s[8:9]
	s_add_u32 s6, s32, 0x3000000
	s_addc_u32 s7, s33, 0
	ds_read_b32 v226, v211
	ds_read_b32 v227, v211 offset:512
	ds_read_b32 v228, v211 offset:1024
	ds_read_b32 v229, v211 offset:1536
	ds_read_b32 v230, v211 offset:2048
	ds_read_b32 v231, v211 offset:2560
	ds_read_b32 v232, v211 offset:3072
	ds_read_b32 v233, v211 offset:3584
	ds_read_b32 v234, v211 offset:4096
	ds_read_b32 v235, v211 offset:4608
	ds_read_b32 v236, v211 offset:5120
	ds_read_b32 v237, v211 offset:5632
	ds_read_b32 v238, v211 offset:6144
	ds_read_b32 v239, v211 offset:6656
	ds_read_b32 v240, v211 offset:7168
	ds_read_b32 v241, v211 offset:7680
	s_waitcnt lgkmcnt(0)
	v_max_f32_e32 v226, v226, v226
	v_max_f32_e32 v227, v227, v227
	v_max_f32_e32 v228, v228, v228
	v_max_f32_e32 v229, v229, v229
	v_max_f32_e32 v230, v230, v230
	v_max_f32_e32 v231, v231, v231
	v_max_f32_e32 v232, v232, v232
	v_max_f32_e32 v233, v233, v233
	v_max_f32_e32 v234, v234, v234
	v_max_f32_e32 v235, v235, v235
	v_max_f32_e32 v236, v236, v236
	v_max_f32_e32 v237, v237, v237
	v_max_f32_e32 v238, v238, v238
	v_max_f32_e32 v239, v239, v239
	v_max_f32_e32 v240, v240, v240
	v_max_f32_e32 v241, v241, v241
	v_med3_f32 v226, v226, s62, v95
	v_med3_f32 v227, v227, s62, v95
	v_med3_f32 v228, v228, s62, v95
	v_med3_f32 v229, v229, s62, v95
	v_med3_f32 v230, v230, s62, v95
	v_med3_f32 v231, v231, s62, v95
	v_med3_f32 v232, v232, s62, v95
	v_med3_f32 v233, v233, s62, v95
	v_med3_f32 v234, v234, s62, v95
	v_med3_f32 v235, v235, s62, v95
	v_med3_f32 v236, v236, s62, v95
	v_med3_f32 v237, v237, s62, v95
	v_med3_f32 v238, v238, s62, v95
	v_med3_f32 v239, v239, s62, v95
	v_med3_f32 v240, v240, s62, v95
	v_med3_f32 v241, v241, s62, v95
	v_mov_b32_e32 v242, 0
	v_mov_b32_e32 v243, 0
	v_mov_b32_e32 v244, 0
	v_mov_b32_e32 v245, 0
	v_cvt_pk_fp8_f32 v242, v226, v227
	v_cvt_pk_fp8_f32 v243, v230, v231
	v_cvt_pk_fp8_f32 v244, v234, v235
	v_cvt_pk_fp8_f32 v245, v238, v239
	v_cvt_pk_fp8_f32 v242, v228, v229 op_sel:[0,0,1]
	v_cvt_pk_fp8_f32 v243, v232, v233 op_sel:[0,0,1]
	v_cvt_pk_fp8_f32 v244, v236, v237 op_sel:[0,0,1]
	v_cvt_pk_fp8_f32 v245, v240, v241 op_sel:[0,0,1]
	s_nop 0
	global_store_dwordx4 v77, v[242:245], s[6:7]
	ds_read_b32 v226, v213
	ds_read_b32 v227, v213 offset:512
	ds_read_b32 v228, v213 offset:1024
	ds_read_b32 v229, v213 offset:1536
	ds_read_b32 v230, v213 offset:2048
	ds_read_b32 v231, v213 offset:2560
	ds_read_b32 v232, v213 offset:3072
	ds_read_b32 v233, v213 offset:3584
	ds_read_b32 v234, v213 offset:4096
	ds_read_b32 v235, v213 offset:4608
	ds_read_b32 v236, v213 offset:5120
	ds_read_b32 v237, v213 offset:5632
	ds_read_b32 v238, v213 offset:6144
	ds_read_b32 v239, v213 offset:6656
	ds_read_b32 v240, v213 offset:7168
	ds_read_b32 v241, v213 offset:7680
	s_waitcnt lgkmcnt(0)
	v_max_f32_e32 v226, v226, v226
	v_max_f32_e32 v227, v227, v227
	v_max_f32_e32 v228, v228, v228
	v_max_f32_e32 v229, v229, v229
	v_max_f32_e32 v230, v230, v230
	v_max_f32_e32 v231, v231, v231
	v_max_f32_e32 v232, v232, v232
	v_max_f32_e32 v233, v233, v233
	v_max_f32_e32 v234, v234, v234
	v_max_f32_e32 v235, v235, v235
	v_max_f32_e32 v236, v236, v236
	v_max_f32_e32 v237, v237, v237
	v_max_f32_e32 v238, v238, v238
	v_max_f32_e32 v239, v239, v239
	v_max_f32_e32 v240, v240, v240
	v_max_f32_e32 v241, v241, v241
	v_med3_f32 v226, v226, s62, v95
	v_med3_f32 v227, v227, s62, v95
	v_med3_f32 v228, v228, s62, v95
	v_med3_f32 v229, v229, s62, v95
	v_med3_f32 v230, v230, s62, v95
	v_med3_f32 v231, v231, s62, v95
	v_med3_f32 v232, v232, s62, v95
	v_med3_f32 v233, v233, s62, v95
	v_med3_f32 v234, v234, s62, v95
	v_med3_f32 v235, v235, s62, v95
	v_med3_f32 v236, v236, s62, v95
	v_med3_f32 v237, v237, s62, v95
	v_med3_f32 v238, v238, s62, v95
	v_med3_f32 v239, v239, s62, v95
	v_med3_f32 v240, v240, s62, v95
	v_med3_f32 v241, v241, s62, v95
	v_mov_b32_e32 v242, 0
	v_mov_b32_e32 v243, 0
	v_mov_b32_e32 v244, 0
	v_mov_b32_e32 v245, 0
	v_cvt_pk_fp8_f32 v242, v226, v227
	v_cvt_pk_fp8_f32 v243, v230, v231
	v_cvt_pk_fp8_f32 v244, v234, v235
	v_cvt_pk_fp8_f32 v245, v238, v239
	v_cvt_pk_fp8_f32 v242, v228, v229 op_sel:[0,0,1]
	v_cvt_pk_fp8_f32 v243, v232, v233 op_sel:[0,0,1]
	v_cvt_pk_fp8_f32 v244, v236, v237 op_sel:[0,0,1]
	v_cvt_pk_fp8_f32 v245, v240, v241 op_sel:[0,0,1]
	s_nop 0
	global_store_dwordx4 v78, v[242:245], s[6:7]
	s_waitcnt vmcnt(12)
	v_mul_f32_e32 v176, v26, v176
	v_mul_f32_e32 v177, v26, v177
	v_mul_f32_e32 v178, v26, v178
	v_mul_f32_e32 v179, v26, v179
	ds_write_b128 v210, v[176:179]
	v_mul_f32_e32 v180, v27, v180
	v_mul_f32_e32 v181, v27, v181
	v_mul_f32_e32 v182, v27, v182
	v_mul_f32_e32 v183, v27, v183
	ds_write_b128 v210, v[180:183] offset:1024
	v_mul_f32_e32 v184, v28, v184
	v_mul_f32_e32 v185, v28, v185
	v_mul_f32_e32 v186, v28, v186
	v_mul_f32_e32 v187, v28, v187
	ds_write_b128 v210, v[184:187] offset:2048
	v_mul_f32_e32 v188, v29, v188
	v_mul_f32_e32 v189, v29, v189
	v_mul_f32_e32 v190, v29, v190
	v_mul_f32_e32 v191, v29, v191
	ds_write_b128 v210, v[188:191] offset:3072
	v_mul_f32_e32 v192, v30, v192
	v_mul_f32_e32 v193, v30, v193
	v_mul_f32_e32 v194, v30, v194
	v_mul_f32_e32 v195, v30, v195
	ds_write_b128 v210, v[192:195] offset:4096
	v_mul_f32_e32 v196, v31, v196
	v_mul_f32_e32 v197, v31, v197
	v_mul_f32_e32 v198, v31, v198
	v_mul_f32_e32 v199, v31, v199
	ds_write_b128 v210, v[196:199] offset:5120
	v_mul_f32_e32 v200, v32, v200
	v_mul_f32_e32 v201, v32, v201
	v_mul_f32_e32 v202, v32, v202
	v_mul_f32_e32 v203, v32, v203
	ds_write_b128 v210, v[200:203] offset:6144
	v_mul_f32_e32 v204, v33, v204
	v_mul_f32_e32 v205, v33, v205
	v_mul_f32_e32 v206, v33, v206
	v_mul_f32_e32 v207, v33, v207
	ds_write_b128 v210, v[204:207] offset:7168
	s_waitcnt lgkmcnt(0)
	s_barrier
; #define GAS __attribute__((address_space(1)))
; #define LAS __attribute__((address_space(3)))
; #define LDS_WAIT() asm volatile("s_waitcnt lgkmcnt(0)" ::: "memory")
; __device__ __forceinline__ unsigned pk4_fp8(float a, float b, float c, float d) {
;     a = fminf(fmaxf(a, -448.f), 448.f); b = fminf(fmaxf(b, -448.f), 448.f); c = fminf(fmaxf(c, -448.f), 448.f); d = fminf(fmaxf(d, -448.f), 448.f);
;     int w = __builtin_amdgcn_cvt_pk_fp8_f32(a, b, 0, false); w = __builtin_amdgcn_cvt_pk_fp8_f32(c, d, w, true); return (unsigned)w; }
;     const int pr = item >> 1, kb = 2 * (pr / nblk) + (item & 1), nb = pr % nblk, k0 = 64 * kb, n0 = 32 * nb;
;     const int nr = n0 + (lane & 31); const int sc = MAP == 1 ? src_col_in(nr) : nr;
;     float v[32];
; #pragma unroll
;     for (int i = 0; i < 32; ++i) v[i] = sc >= 0 ? W[(size_t)(k0 + 2 * i + (lane >> 5)) * Nsrc + sc] : 0.f;
; #pragma unroll
;     for (int i = 0; i < 32; ++i) { const int k = k0 + 2 * i + (lane >> 5); float x = v[i] * wscale; if (KS) x *= (k < ksplit ? ksA[k] : ksB[k - ksplit]); scr[(2 * i + (lane >> 5)) * 33 + (lane & 31)] = x; }
;     LDS_WAIT(); asm volatile("" ::: "memory");
;     const int c = lane & 7;
; #pragma unroll
;     for (int j = 0; j < 4; ++j) { const int n = (lane >> 3) + 8 * j; const LAS float* s = scr + (8 * c) * 33 + n;
;         const unsigned long long o = (unsigned long long)pg8::pk4_fp8(s[0 * 33], s[1 * 33], s[2 * 33], s[3 * 33]) | ((unsigned long long)pg8::pk4_fp8(s[4 * 33], s[5 * 33], s[6 * 33], s[7 * 33]) << 32);
;         *(GAS unsigned long long*)(WT + (size_t)(n0 + n) * K + k0 + 8 * c) = o; }
;     LDS_WAIT(); asm volatile("" ::: "memory");
	s_add_u32 s8, s30, 0xf000
	s_addc_u32 s9, s31, 0
	global_load_dwordx4 v[176:179], v74, s[8:9]
	s_add_u32 s8, s8, 0x20000
	s_addc_u32 s9, s9, 0
	global_load_dwordx4 v[180:183], v74, s[8:9]
	s_add_u32 s8, s8, 0x20000
	s_addc_u32 s9, s9, 0
	global_load_dwordx4 v[184:187], v74, s[8:9]
	s_add_u32 s8, s8, 0x20000
	s_addc_u32 s9, s9, 0
	global_load_dwordx4 v[188:191], v74, s[8:9]
	s_add_u32 s8, s8, 0x20000
	s_addc_u32 s9, s9, 0
	global_load_dwordx4 v[192:195], v74, s[8:9]
	s_add_u32 s8, s8, 0x20000
	s_addc_u32 s9, s9, 0
	global_load_dwordx4 v[196:199], v74, s[8:9]
	s_add_u32 s8, s8, 0x20000
	s_addc_u32 s9, s9, 0
	global_load_dwordx4 v[200:203], v74, s[8:9]
	s_add_u32 s8, s8, 0x20000
	s_addc_u32 s9, s9, 0
	global_load_dwordx4 v[204:207], v74, s[8:9]
	s_add_u32 s6, s32, 0x3400000
	s_addc_u32 s7, s33, 0
	ds_read_b32 v226, v212
	ds_read_b32 v227, v212 offset:512
	ds_read_b32 v228, v212 offset:1024
	ds_read_b32 v229, v212 offset:1536
	ds_read_b32 v230, v212 offset:2048
	ds_read_b32 v231, v212 offset:2560
	ds_read_b32 v232, v212 offset:3072
	ds_read_b32 v233, v212 offset:3584
	ds_read_b32 v234, v212 offset:4096
	ds_read_b32 v235, v212 offset:4608
	ds_read_b32 v236, v212 offset:5120
	ds_read_b32 v237, v212 offset:5632
	ds_read_b32 v238, v212 offset:6144
	ds_read_b32 v239, v212 offset:6656
	ds_read_b32 v240, v212 offset:7168
	ds_read_b32 v241, v212 offset:7680
	s_waitcnt lgkmcnt(0)
	v_max_f32_e32 v226, v226, v226
	v_max_f32_e32 v227, v227, v227
	v_max_f32_e32 v228, v228, v228
	v_max_f32_e32 v229, v229, v229
	v_max_f32_e32 v230, v230, v230
	v_max_f32_e32 v231, v231, v231
	v_max_f32_e32 v232, v232, v232
	v_max_f32_e32 v233, v233, v233
	v_max_f32_e32 v234, v234, v234
	v_max_f32_e32 v235, v235, v235
	v_max_f32_e32 v236, v236, v236
	v_max_f32_e32 v237, v237, v237
	v_max_f32_e32 v238, v238, v238
	v_max_f32_e32 v239, v239, v239
	v_max_f32_e32 v240, v240, v240
	v_max_f32_e32 v241, v241, v241
	v_med3_f32 v226, v226, s62, v95
	v_med3_f32 v227, v227, s62, v95
	v_med3_f32 v228, v228, s62, v95
	v_med3_f32 v229, v229, s62, v95
	v_med3_f32 v230, v230, s62, v95
	v_med3_f32 v231, v231, s62, v95
	v_med3_f32 v232, v232, s62, v95
	v_med3_f32 v233, v233, s62, v95
	v_med3_f32 v234, v234, s62, v95
	v_med3_f32 v235, v235, s62, v95
	v_med3_f32 v236, v236, s62, v95
	v_med3_f32 v237, v237, s62, v95
	v_med3_f32 v238, v238, s62, v95
	v_med3_f32 v239, v239, s62, v95
	v_med3_f32 v240, v240, s62, v95
	v_med3_f32 v241, v241, s62, v95
	v_mov_b32_e32 v242, 0
	v_mov_b32_e32 v243, 0
	v_mov_b32_e32 v244, 0
	v_mov_b32_e32 v245, 0
	v_cvt_pk_fp8_f32 v242, v226, v227
	v_cvt_pk_fp8_f32 v243, v230, v231
	v_cvt_pk_fp8_f32 v244, v234, v235
	v_cvt_pk_fp8_f32 v245, v238, v239
	v_cvt_pk_fp8_f32 v242, v228, v229 op_sel:[0,0,1]
	v_cvt_pk_fp8_f32 v243, v232, v233 op_sel:[0,0,1]
	v_cvt_pk_fp8_f32 v244, v236, v237 op_sel:[0,0,1]
	v_cvt_pk_fp8_f32 v245, v240, v241 op_sel:[0,0,1]
	s_nop 0
	global_store_dwordx4 v77, v[242:245], s[6:7]
	ds_read_b32 v226, v214
	ds_read_b32 v227, v214 offset:512
	ds_read_b32 v228, v214 offset:1024
	ds_read_b32 v229, v214 offset:1536
	ds_read_b32 v230, v214 offset:2048
	ds_read_b32 v231, v214 offset:2560
	ds_read_b32 v232, v214 offset:3072
	ds_read_b32 v233, v214 offset:3584
	ds_read_b32 v234, v214 offset:4096
	ds_read_b32 v235, v214 offset:4608
	ds_read_b32 v236, v214 offset:5120
	ds_read_b32 v237, v214 offset:5632
	ds_read_b32 v238, v214 offset:6144
	ds_read_b32 v239, v214 offset:6656
	ds_read_b32 v240, v214 offset:7168
	ds_read_b32 v241, v214 offset:7680
	s_waitcnt lgkmcnt(0)
	v_max_f32_e32 v226, v226, v226
	v_max_f32_e32 v227, v227, v227
	v_max_f32_e32 v228, v228, v228
	v_max_f32_e32 v229, v229, v229
	v_max_f32_e32 v230, v230, v230
	v_max_f32_e32 v231, v231, v231
	v_max_f32_e32 v232, v232, v232
	v_max_f32_e32 v233, v233, v233
	v_max_f32_e32 v234, v234, v234
	v_max_f32_e32 v235, v235, v235
	v_max_f32_e32 v236, v236, v236
	v_max_f32_e32 v237, v237, v237
	v_max_f32_e32 v238, v238, v238
	v_max_f32_e32 v239, v239, v239
	v_max_f32_e32 v240, v240, v240
	v_max_f32_e32 v241, v241, v241
	v_med3_f32 v226, v226, s62, v95
	v_med3_f32 v227, v227, s62, v95
	v_med3_f32 v228, v228, s62, v95
	v_med3_f32 v229, v229, s62, v95
	v_med3_f32 v230, v230, s62, v95
	v_med3_f32 v231, v231, s62, v95
	v_med3_f32 v232, v232, s62, v95
	v_med3_f32 v233, v233, s62, v95
	v_med3_f32 v234, v234, s62, v95
	v_med3_f32 v235, v235, s62, v95
	v_med3_f32 v236, v236, s62, v95
	v_med3_f32 v237, v237, s62, v95
	v_med3_f32 v238, v238, s62, v95
	v_med3_f32 v239, v239, s62, v95
	v_med3_f32 v240, v240, s62, v95
	v_med3_f32 v241, v241, s62, v95
	v_mov_b32_e32 v242, 0
	v_mov_b32_e32 v243, 0
	v_mov_b32_e32 v244, 0
	v_mov_b32_e32 v245, 0
	v_cvt_pk_fp8_f32 v242, v226, v227
	v_cvt_pk_fp8_f32 v243, v230, v231
	v_cvt_pk_fp8_f32 v244, v234, v235
	v_cvt_pk_fp8_f32 v245, v238, v239
	v_cvt_pk_fp8_f32 v242, v228, v229 op_sel:[0,0,1]
	v_cvt_pk_fp8_f32 v243, v232, v233 op_sel:[0,0,1]
	v_cvt_pk_fp8_f32 v244, v236, v237 op_sel:[0,0,1]
	v_cvt_pk_fp8_f32 v245, v240, v241 op_sel:[0,0,1]
	s_nop 0
	global_store_dwordx4 v78, v[242:245], s[6:7]
	s_waitcnt vmcnt(12)
	v_mul_f32_e32 v144, v26, v144
	v_mul_f32_e32 v145, v26, v145
	v_mul_f32_e32 v146, v26, v146
	v_mul_f32_e32 v147, v26, v147
	ds_write_b128 v209, v[144:147]
	v_mul_f32_e32 v148, v27, v148
	v_mul_f32_e32 v149, v27, v149
	v_mul_f32_e32 v150, v27, v150
	v_mul_f32_e32 v151, v27, v151
	ds_write_b128 v209, v[148:151] offset:1024
	v_mul_f32_e32 v152, v28, v152
	v_mul_f32_e32 v153, v28, v153
	v_mul_f32_e32 v154, v28, v154
	v_mul_f32_e32 v155, v28, v155
	ds_write_b128 v209, v[152:155] offset:2048
	v_mul_f32_e32 v156, v29, v156
	v_mul_f32_e32 v157, v29, v157
	v_mul_f32_e32 v158, v29, v158
	v_mul_f32_e32 v159, v29, v159
	ds_write_b128 v209, v[156:159] offset:3072
	v_mul_f32_e32 v160, v30, v160
	v_mul_f32_e32 v161, v30, v161
	v_mul_f32_e32 v162, v30, v162
	v_mul_f32_e32 v163, v30, v163
	ds_write_b128 v209, v[160:163] offset:4096
	v_mul_f32_e32 v164, v31, v164
	v_mul_f32_e32 v165, v31, v165
	v_mul_f32_e32 v166, v31, v166
	v_mul_f32_e32 v167, v31, v167
	ds_write_b128 v209, v[164:167] offset:5120
	v_mul_f32_e32 v168, v32, v168
	v_mul_f32_e32 v169, v32, v169
	v_mul_f32_e32 v170, v32, v170
	v_mul_f32_e32 v171, v32, v171
	ds_write_b128 v209, v[168:171] offset:6144
	v_mul_f32_e32 v172, v33, v172
	v_mul_f32_e32 v173, v33, v173
	v_mul_f32_e32 v174, v33, v174
	v_mul_f32_e32 v175, v33, v175
	ds_write_b128 v209, v[172:175] offset:7168
	s_waitcnt lgkmcnt(0)
	s_barrier
; #define GAS __attribute__((address_space(1)))
; #define LAS __attribute__((address_space(3)))
; #define LDS_WAIT() asm volatile("s_waitcnt lgkmcnt(0)" ::: "memory")
; __device__ __forceinline__ unsigned pk4_fp8(float a, float b, float c, float d) {
;     a = fminf(fmaxf(a, -448.f), 448.f); b = fminf(fmaxf(b, -448.f), 448.f); c = fminf(fmaxf(c, -448.f), 448.f); d = fminf(fmaxf(d, -448.f), 448.f);
;     int w = __builtin_amdgcn_cvt_pk_fp8_f32(a, b, 0, false); w = __builtin_amdgcn_cvt_pk_fp8_f32(c, d, w, true); return (unsigned)w; }
;     const int pr = item >> 1, kb = 2 * (pr / nblk) + (item & 1), nb = pr % nblk, k0 = 64 * kb, n0 = 32 * nb;
;     const int nr = n0 + (lane & 31); const int sc = MAP == 1 ? src_col_in(nr) : nr;
;     float v[32];
; #pragma unroll
;     for (int i = 0; i < 32; ++i) v[i] = sc >= 0 ? W[(size_t)(k0 + 2 * i + (lane >> 5)) * Nsrc + sc] : 0.f;
; #pragma unroll
;     for (int i = 0; i < 32; ++i) { const int k = k0 + 2 * i + (lane >> 5); float x = v[i] * wscale; if (KS) x *= (k < ksplit ? ksA[k] : ksB[k - ksplit]); scr[(2 * i + (lane >> 5)) * 33 + (lane & 31)] = x; }
;     LDS_WAIT(); asm volatile("" ::: "memory");
;     const int c = lane & 7;
; #pragma unroll
;     for (int j = 0; j < 4; ++j) { const int n = (lane >> 3) + 8 * j; const LAS float* s = scr + (8 * c) * 33 + n;
;         const unsigned long long o = (unsigned long long)pg8::pk4_fp8(s[0 * 33], s[1 * 33], s[2 * 33], s[3 * 33]) | ((unsigned long long)pg8::pk4_fp8(s[4 * 33], s[5 * 33], s[6 * 33], s[7 * 33]) << 32);
;         *(GAS unsigned long long*)(WT + (size_t)(n0 + n) * K + k0 + 8 * c) = o; }
;     LDS_WAIT(); asm volatile("" ::: "memory");
	s_mov_b64 s[8:9], s[34:35]
	global_load_dwordx4 v[144:147], v74, s[8:9]
	s_add_u32 s8, s8, 0x20000
	s_addc_u32 s9, s9, 0
	global_load_dwordx4 v[148:151], v74, s[8:9]
	s_add_u32 s8, s8, 0x20000
	s_addc_u32 s9, s9, 0
	global_load_dwordx4 v[152:155], v74, s[8:9]
	s_add_u32 s8, s8, 0x20000
	s_addc_u32 s9, s9, 0
	global_load_dwordx4 v[156:159], v74, s[8:9]
	s_add_u32 s8, s8, 0x20000
	s_addc_u32 s9, s9, 0
	global_load_dwordx4 v[160:163], v74, s[8:9]
	s_add_u32 s8, s8, 0x20000
	s_addc_u32 s9, s9, 0
	global_load_dwordx4 v[164:167], v74, s[8:9]
	s_add_u32 s8, s8, 0x20000
	s_addc_u32 s9, s9, 0
	global_load_dwordx4 v[168:171], v74, s[8:9]
	s_add_u32 s8, s8, 0x20000
	s_addc_u32 s9, s9, 0
	global_load_dwordx4 v[172:175], v74, s[8:9]
	s_add_u32 s6, s32, 0x3800000
	s_addc_u32 s7, s33, 0
	ds_read_b32 v226, v211
	ds_read_b32 v227, v211 offset:512
	ds_read_b32 v228, v211 offset:1024
	ds_read_b32 v229, v211 offset:1536
	ds_read_b32 v230, v211 offset:2048
	ds_read_b32 v231, v211 offset:2560
	ds_read_b32 v232, v211 offset:3072
	ds_read_b32 v233, v211 offset:3584
	ds_read_b32 v234, v211 offset:4096
	ds_read_b32 v235, v211 offset:4608
	ds_read_b32 v236, v211 offset:5120
	ds_read_b32 v237, v211 offset:5632
	ds_read_b32 v238, v211 offset:6144
	ds_read_b32 v239, v211 offset:6656
	ds_read_b32 v240, v211 offset:7168
	ds_read_b32 v241, v211 offset:7680
	s_waitcnt lgkmcnt(0)
	v_max_f32_e32 v226, v226, v226
	v_max_f32_e32 v227, v227, v227
	v_max_f32_e32 v228, v228, v228
	v_max_f32_e32 v229, v229, v229
	v_max_f32_e32 v230, v230, v230
	v_max_f32_e32 v231, v231, v231
	v_max_f32_e32 v232, v232, v232
	v_max_f32_e32 v233, v233, v233
	v_max_f32_e32 v234, v234, v234
	v_max_f32_e32 v235, v235, v235
	v_max_f32_e32 v236, v236, v236
	v_max_f32_e32 v237, v237, v237
	v_max_f32_e32 v238, v238, v238
	v_max_f32_e32 v239, v239, v239
	v_max_f32_e32 v240, v240, v240
	v_max_f32_e32 v241, v241, v241
	v_med3_f32 v226, v226, s62, v95
	v_med3_f32 v227, v227, s62, v95
	v_med3_f32 v228, v228, s62, v95
	v_med3_f32 v229, v229, s62, v95
	v_med3_f32 v230, v230, s62, v95
	v_med3_f32 v231, v231, s62, v95
	v_med3_f32 v232, v232, s62, v95
	v_med3_f32 v233, v233, s62, v95
	v_med3_f32 v234, v234, s62, v95
	v_med3_f32 v235, v235, s62, v95
	v_med3_f32 v236, v236, s62, v95
	v_med3_f32 v237, v237, s62, v95
	v_med3_f32 v238, v238, s62, v95
	v_med3_f32 v239, v239, s62, v95
	v_med3_f32 v240, v240, s62, v95
	v_med3_f32 v241, v241, s62, v95
	v_mov_b32_e32 v242, 0
	v_mov_b32_e32 v243, 0
	v_mov_b32_e32 v244, 0
	v_mov_b32_e32 v245, 0
	v_cvt_pk_fp8_f32 v242, v226, v227
	v_cvt_pk_fp8_f32 v243, v230, v231
	v_cvt_pk_fp8_f32 v244, v234, v235
	v_cvt_pk_fp8_f32 v245, v238, v239
	v_cvt_pk_fp8_f32 v242, v228, v229 op_sel:[0,0,1]
	v_cvt_pk_fp8_f32 v243, v232, v233 op_sel:[0,0,1]
	v_cvt_pk_fp8_f32 v244, v236, v237 op_sel:[0,0,1]
	v_cvt_pk_fp8_f32 v245, v240, v241 op_sel:[0,0,1]
	s_nop 0
	global_store_dwordx4 v77, v[242:245], s[6:7]
	ds_read_b32 v226, v213
	ds_read_b32 v227, v213 offset:512
	ds_read_b32 v228, v213 offset:1024
	ds_read_b32 v229, v213 offset:1536
	ds_read_b32 v230, v213 offset:2048
	ds_read_b32 v231, v213 offset:2560
	ds_read_b32 v232, v213 offset:3072
	ds_read_b32 v233, v213 offset:3584
	ds_read_b32 v234, v213 offset:4096
	ds_read_b32 v235, v213 offset:4608
	ds_read_b32 v236, v213 offset:5120
	ds_read_b32 v237, v213 offset:5632
	ds_read_b32 v238, v213 offset:6144
	ds_read_b32 v239, v213 offset:6656
	ds_read_b32 v240, v213 offset:7168
	ds_read_b32 v241, v213 offset:7680
	s_waitcnt lgkmcnt(0)
	v_max_f32_e32 v226, v226, v226
	v_max_f32_e32 v227, v227, v227
	v_max_f32_e32 v228, v228, v228
	v_max_f32_e32 v229, v229, v229
	v_max_f32_e32 v230, v230, v230
	v_max_f32_e32 v231, v231, v231
	v_max_f32_e32 v232, v232, v232
	v_max_f32_e32 v233, v233, v233
	v_max_f32_e32 v234, v234, v234
	v_max_f32_e32 v235, v235, v235
	v_max_f32_e32 v236, v236, v236
	v_max_f32_e32 v237, v237, v237
	v_max_f32_e32 v238, v238, v238
	v_max_f32_e32 v239, v239, v239
	v_max_f32_e32 v240, v240, v240
	v_max_f32_e32 v241, v241, v241
	v_med3_f32 v226, v226, s62, v95
	v_med3_f32 v227, v227, s62, v95
	v_med3_f32 v228, v228, s62, v95
	v_med3_f32 v229, v229, s62, v95
	v_med3_f32 v230, v230, s62, v95
	v_med3_f32 v231, v231, s62, v95
	v_med3_f32 v232, v232, s62, v95
	v_med3_f32 v233, v233, s62, v95
	v_med3_f32 v234, v234, s62, v95
	v_med3_f32 v235, v235, s62, v95
	v_med3_f32 v236, v236, s62, v95
	v_med3_f32 v237, v237, s62, v95
	v_med3_f32 v238, v238, s62, v95
	v_med3_f32 v239, v239, s62, v95
	v_med3_f32 v240, v240, s62, v95
	v_med3_f32 v241, v241, s62, v95
	v_mov_b32_e32 v242, 0
	v_mov_b32_e32 v243, 0
	v_mov_b32_e32 v244, 0
	v_mov_b32_e32 v245, 0
	v_cvt_pk_fp8_f32 v242, v226, v227
	v_cvt_pk_fp8_f32 v243, v230, v231
	v_cvt_pk_fp8_f32 v244, v234, v235
	v_cvt_pk_fp8_f32 v245, v238, v239
	v_cvt_pk_fp8_f32 v242, v228, v229 op_sel:[0,0,1]
	v_cvt_pk_fp8_f32 v243, v232, v233 op_sel:[0,0,1]
	v_cvt_pk_fp8_f32 v244, v236, v237 op_sel:[0,0,1]
	v_cvt_pk_fp8_f32 v245, v240, v241 op_sel:[0,0,1]
	s_nop 0
	global_store_dwordx4 v78, v[242:245], s[6:7]
	s_waitcnt vmcnt(12)
	v_mul_f32_e32 v176, v26, v176
	v_mul_f32_e32 v177, v26, v177
	v_mul_f32_e32 v178, v26, v178
	v_mul_f32_e32 v179, v26, v179
	ds_write_b128 v210, v[176:179]
	v_mul_f32_e32 v180, v27, v180
	v_mul_f32_e32 v181, v27, v181
	v_mul_f32_e32 v182, v27, v182
	v_mul_f32_e32 v183, v27, v183
	ds_write_b128 v210, v[180:183] offset:1024
	v_mul_f32_e32 v184, v28, v184
	v_mul_f32_e32 v185, v28, v185
	v_mul_f32_e32 v186, v28, v186
	v_mul_f32_e32 v187, v28, v187
	ds_write_b128 v210, v[184:187] offset:2048
	v_mul_f32_e32 v188, v29, v188
	v_mul_f32_e32 v189, v29, v189
	v_mul_f32_e32 v190, v29, v190
	v_mul_f32_e32 v191, v29, v191
	ds_write_b128 v210, v[188:191] offset:3072
	v_mul_f32_e32 v192, v30, v192
	v_mul_f32_e32 v193, v30, v193
	v_mul_f32_e32 v194, v30, v194
	v_mul_f32_e32 v195, v30, v195
	ds_write_b128 v210, v[192:195] offset:4096
	v_mul_f32_e32 v196, v31, v196
	v_mul_f32_e32 v197, v31, v197
	v_mul_f32_e32 v198, v31, v198
	v_mul_f32_e32 v199, v31, v199
	ds_write_b128 v210, v[196:199] offset:5120
	v_mul_f32_e32 v200, v32, v200
	v_mul_f32_e32 v201, v32, v201
	v_mul_f32_e32 v202, v32, v202
	v_mul_f32_e32 v203, v32, v203
	ds_write_b128 v210, v[200:203] offset:6144
	v_mul_f32_e32 v204, v33, v204
	v_mul_f32_e32 v205, v33, v205
	v_mul_f32_e32 v206, v33, v206
	v_mul_f32_e32 v207, v33, v207
	ds_write_b128 v210, v[204:207] offset:7168
	s_waitcnt lgkmcnt(0)
	s_barrier
; #define GAS __attribute__((address_space(1)))
; #define LAS __attribute__((address_space(3)))
; #define LDS_WAIT() asm volatile("s_waitcnt lgkmcnt(0)" ::: "memory")
; __device__ __forceinline__ unsigned pk4_fp8(float a, float b, float c, float d) {
;     a = fminf(fmaxf(a, -448.f), 448.f); b = fminf(fmaxf(b, -448.f), 448.f); c = fminf(fmaxf(c, -448.f), 448.f); d = fminf(fmaxf(d, -448.f), 448.f);
;     int w = __builtin_amdgcn_cvt_pk_fp8_f32(a, b, 0, false); w = __builtin_amdgcn_cvt_pk_fp8_f32(c, d, w, true); return (unsigned)w; }
;     const int pr = item >> 1, kb = 2 * (pr / nblk) + (item & 1), nb = pr % nblk, k0 = 64 * kb, n0 = 32 * nb;
;     const int nr = n0 + (lane & 31); const int sc = MAP == 1 ? src_col_in(nr) : nr;
;     float v[32];
; #pragma unroll
;     for (int i = 0; i < 32; ++i) v[i] = sc >= 0 ? W[(size_t)(k0 + 2 * i + (lane >> 5)) * Nsrc + sc] : 0.f;
; #pragma unroll
;     for (int i = 0; i < 32; ++i) { const int k = k0 + 2 * i + (lane >> 5); float x = v[i] * wscale; if (KS) x *= (k < ksplit ? ksA[k] : ksB[k - ksplit]); scr[(2 * i + (lane >> 5)) * 33 + (lane & 31)] = x; }
;     LDS_WAIT(); asm volatile("" ::: "memory");
;     const int c = lane & 7;
; #pragma unroll
;     for (int j = 0; j < 4; ++j) { const int n = (lane >> 3) + 8 * j; const LAS float* s = scr + (8 * c) * 33 + n;
;         const unsigned long long o = (unsigned long long)pg8::pk4_fp8(s[0 * 33], s[1 * 33], s[2 * 33], s[3 * 33]) | ((unsigned long long)pg8::pk4_fp8(s[4 * 33], s[5 * 33], s[6 * 33], s[7 * 33]) << 32);
;         *(GAS unsigned long long*)(WT + (size_t)(n0 + n) * K + k0 + 8 * c) = o; }
;     LDS_WAIT(); asm volatile("" ::: "memory");
	s_add_u32 s8, s34, 0x1000
	s_addc_u32 s9, s35, 0
	global_load_dwordx4 v[176:179], v74, s[8:9]
	s_add_u32 s8, s8, 0x20000
	s_addc_u32 s9, s9, 0
	global_load_dwordx4 v[180:183], v74, s[8:9]
	s_add_u32 s8, s8, 0x20000
	s_addc_u32 s9, s9, 0
	global_load_dwordx4 v[184:187], v74, s[8:9]
	s_add_u32 s8, s8, 0x20000
	s_addc_u32 s9, s9, 0
	global_load_dwordx4 v[188:191], v74, s[8:9]
	s_add_u32 s8, s8, 0x20000
	s_addc_u32 s9, s9, 0
	global_load_dwordx4 v[192:195], v74, s[8:9]
	s_add_u32 s8, s8, 0x20000
	s_addc_u32 s9, s9, 0
	global_load_dwordx4 v[196:199], v74, s[8:9]
	s_add_u32 s8, s8, 0x20000
	s_addc_u32 s9, s9, 0
	global_load_dwordx4 v[200:203], v74, s[8:9]
	s_add_u32 s8, s8, 0x20000
	s_addc_u32 s9, s9, 0
	global_load_dwordx4 v[204:207], v74, s[8:9]
	s_add_u32 s6, s32, 0x3c00000
	s_addc_u32 s7, s33, 0
	ds_read_b32 v226, v212
	ds_read_b32 v227, v212 offset:512
	ds_read_b32 v228, v212 offset:1024
	ds_read_b32 v229, v212 offset:1536
	ds_read_b32 v230, v212 offset:2048
	ds_read_b32 v231, v212 offset:2560
	ds_read_b32 v232, v212 offset:3072
	ds_read_b32 v233, v212 offset:3584
	ds_read_b32 v234, v212 offset:4096
	ds_read_b32 v235, v212 offset:4608
	ds_read_b32 v236, v212 offset:5120
	ds_read_b32 v237, v212 offset:5632
	ds_read_b32 v238, v212 offset:6144
	ds_read_b32 v239, v212 offset:6656
	ds_read_b32 v240, v212 offset:7168
	ds_read_b32 v241, v212 offset:7680
	s_waitcnt lgkmcnt(0)
	v_max_f32_e32 v226, v226, v226
	v_max_f32_e32 v227, v227, v227
	v_max_f32_e32 v228, v228, v228
	v_max_f32_e32 v229, v229, v229
	v_max_f32_e32 v230, v230, v230
	v_max_f32_e32 v231, v231, v231
	v_max_f32_e32 v232, v232, v232
	v_max_f32_e32 v233, v233, v233
	v_max_f32_e32 v234, v234, v234
	v_max_f32_e32 v235, v235, v235
	v_max_f32_e32 v236, v236, v236
	v_max_f32_e32 v237, v237, v237
	v_max_f32_e32 v238, v238, v238
	v_max_f32_e32 v239, v239, v239
	v_max_f32_e32 v240, v240, v240
	v_max_f32_e32 v241, v241, v241
	v_med3_f32 v226, v226, s62, v95
	v_med3_f32 v227, v227, s62, v95
	v_med3_f32 v228, v228, s62, v95
	v_med3_f32 v229, v229, s62, v95
	v_med3_f32 v230, v230, s62, v95
	v_med3_f32 v231, v231, s62, v95
	v_med3_f32 v232, v232, s62, v95
	v_med3_f32 v233, v233, s62, v95
	v_med3_f32 v234, v234, s62, v95
	v_med3_f32 v235, v235, s62, v95
	v_med3_f32 v236, v236, s62, v95
	v_med3_f32 v237, v237, s62, v95
	v_med3_f32 v238, v238, s62, v95
	v_med3_f32 v239, v239, s62, v95
	v_med3_f32 v240, v240, s62, v95
	v_med3_f32 v241, v241, s62, v95
	v_mov_b32_e32 v242, 0
	v_mov_b32_e32 v243, 0
	v_mov_b32_e32 v244, 0
	v_mov_b32_e32 v245, 0
	v_cvt_pk_fp8_f32 v242, v226, v227
	v_cvt_pk_fp8_f32 v243, v230, v231
	v_cvt_pk_fp8_f32 v244, v234, v235
	v_cvt_pk_fp8_f32 v245, v238, v239
	v_cvt_pk_fp8_f32 v242, v228, v229 op_sel:[0,0,1]
	v_cvt_pk_fp8_f32 v243, v232, v233 op_sel:[0,0,1]
	v_cvt_pk_fp8_f32 v244, v236, v237 op_sel:[0,0,1]
	v_cvt_pk_fp8_f32 v245, v240, v241 op_sel:[0,0,1]
	s_nop 0
	global_store_dwordx4 v77, v[242:245], s[6:7]
	ds_read_b32 v226, v214
	ds_read_b32 v227, v214 offset:512
	ds_read_b32 v228, v214 offset:1024
	ds_read_b32 v229, v214 offset:1536
	ds_read_b32 v230, v214 offset:2048
	ds_read_b32 v231, v214 offset:2560
	ds_read_b32 v232, v214 offset:3072
	ds_read_b32 v233, v214 offset:3584
	ds_read_b32 v234, v214 offset:4096
	ds_read_b32 v235, v214 offset:4608
	ds_read_b32 v236, v214 offset:5120
	ds_read_b32 v237, v214 offset:5632
	ds_read_b32 v238, v214 offset:6144
	ds_read_b32 v239, v214 offset:6656
	ds_read_b32 v240, v214 offset:7168
	ds_read_b32 v241, v214 offset:7680
	s_waitcnt lgkmcnt(0)
	v_max_f32_e32 v226, v226, v226
	v_max_f32_e32 v227, v227, v227
	v_max_f32_e32 v228, v228, v228
	v_max_f32_e32 v229, v229, v229
	v_max_f32_e32 v230, v230, v230
	v_max_f32_e32 v231, v231, v231
	v_max_f32_e32 v232, v232, v232
	v_max_f32_e32 v233, v233, v233
	v_max_f32_e32 v234, v234, v234
	v_max_f32_e32 v235, v235, v235
	v_max_f32_e32 v236, v236, v236
	v_max_f32_e32 v237, v237, v237
	v_max_f32_e32 v238, v238, v238
	v_max_f32_e32 v239, v239, v239
	v_max_f32_e32 v240, v240, v240
	v_max_f32_e32 v241, v241, v241
	v_med3_f32 v226, v226, s62, v95
	v_med3_f32 v227, v227, s62, v95
	v_med3_f32 v228, v228, s62, v95
	v_med3_f32 v229, v229, s62, v95
	v_med3_f32 v230, v230, s62, v95
	v_med3_f32 v231, v231, s62, v95
	v_med3_f32 v232, v232, s62, v95
	v_med3_f32 v233, v233, s62, v95
	v_med3_f32 v234, v234, s62, v95
	v_med3_f32 v235, v235, s62, v95
	v_med3_f32 v236, v236, s62, v95
	v_med3_f32 v237, v237, s62, v95
	v_med3_f32 v238, v238, s62, v95
	v_med3_f32 v239, v239, s62, v95
	v_med3_f32 v240, v240, s62, v95
	v_med3_f32 v241, v241, s62, v95
	v_mov_b32_e32 v242, 0
	v_mov_b32_e32 v243, 0
	v_mov_b32_e32 v244, 0
	v_mov_b32_e32 v245, 0
	v_cvt_pk_fp8_f32 v242, v226, v227
	v_cvt_pk_fp8_f32 v243, v230, v231
	v_cvt_pk_fp8_f32 v244, v234, v235
	v_cvt_pk_fp8_f32 v245, v238, v239
	v_cvt_pk_fp8_f32 v242, v228, v229 op_sel:[0,0,1]
	v_cvt_pk_fp8_f32 v243, v232, v233 op_sel:[0,0,1]
	v_cvt_pk_fp8_f32 v244, v236, v237 op_sel:[0,0,1]
	v_cvt_pk_fp8_f32 v245, v240, v241 op_sel:[0,0,1]
	s_nop 0
	global_store_dwordx4 v78, v[242:245], s[6:7]
	s_waitcnt vmcnt(12)
	v_mul_f32_e32 v144, v34, v144
	v_mul_f32_e32 v145, v34, v145
	v_mul_f32_e32 v146, v34, v146
	v_mul_f32_e32 v147, v34, v147
	ds_write_b128 v209, v[144:147]
	v_mul_f32_e32 v148, v35, v148
	v_mul_f32_e32 v149, v35, v149
	v_mul_f32_e32 v150, v35, v150
	v_mul_f32_e32 v151, v35, v151
	ds_write_b128 v209, v[148:151] offset:1024
	v_mul_f32_e32 v152, v36, v152
	v_mul_f32_e32 v153, v36, v153
	v_mul_f32_e32 v154, v36, v154
	v_mul_f32_e32 v155, v36, v155
	ds_write_b128 v209, v[152:155] offset:2048
	v_mul_f32_e32 v156, v37, v156
	v_mul_f32_e32 v157, v37, v157
	v_mul_f32_e32 v158, v37, v158
	v_mul_f32_e32 v159, v37, v159
	ds_write_b128 v209, v[156:159] offset:3072
	v_mul_f32_e32 v160, v38, v160
	v_mul_f32_e32 v161, v38, v161
	v_mul_f32_e32 v162, v38, v162
	v_mul_f32_e32 v163, v38, v163
	ds_write_b128 v209, v[160:163] offset:4096
	v_mul_f32_e32 v164, v39, v164
	v_mul_f32_e32 v165, v39, v165
	v_mul_f32_e32 v166, v39, v166
	v_mul_f32_e32 v167, v39, v167
	ds_write_b128 v209, v[164:167] offset:5120
	v_mul_f32_e32 v168, v40, v168
	v_mul_f32_e32 v169, v40, v169
	v_mul_f32_e32 v170, v40, v170
	v_mul_f32_e32 v171, v40, v171
	ds_write_b128 v209, v[168:171] offset:6144
	v_mul_f32_e32 v172, v41, v172
	v_mul_f32_e32 v173, v41, v173
	v_mul_f32_e32 v174, v41, v174
	v_mul_f32_e32 v175, v41, v175
	ds_write_b128 v209, v[172:175] offset:7168
	s_waitcnt lgkmcnt(0)
	s_barrier
; #define GAS __attribute__((address_space(1)))
; #define LAS __attribute__((address_space(3)))
; #define LDS_WAIT() asm volatile("s_waitcnt lgkmcnt(0)" ::: "memory")
; __device__ __forceinline__ unsigned pk4_fp8(float a, float b, float c, float d) {
;     a = fminf(fmaxf(a, -448.f), 448.f); b = fminf(fmaxf(b, -448.f), 448.f); c = fminf(fmaxf(c, -448.f), 448.f); d = fminf(fmaxf(d, -448.f), 448.f);
;     int w = __builtin_amdgcn_cvt_pk_fp8_f32(a, b, 0, false); w = __builtin_amdgcn_cvt_pk_fp8_f32(c, d, w, true); return (unsigned)w; }
;     const int pr = item >> 1, kb = 2 * (pr / nblk) + (item & 1), nb = pr % nblk, k0 = 64 * kb, n0 = 32 * nb;
;     const int nr = n0 + (lane & 31); const int sc = MAP == 1 ? src_col_in(nr) : nr;
;     float v[32];
; #pragma unroll
;     for (int i = 0; i < 32; ++i) v[i] = sc >= 0 ? W[(size_t)(k0 + 2 * i + (lane >> 5)) * Nsrc + sc] : 0.f;
; #pragma unroll
;     for (int i = 0; i < 32; ++i) { const int k = k0 + 2 * i + (lane >> 5); float x = v[i] * wscale; if (KS) x *= (k < ksplit ? ksA[k] : ksB[k - ksplit]); scr[(2 * i + (lane >> 5)) * 33 + (lane & 31)] = x; }
;     LDS_WAIT(); asm volatile("" ::: "memory");
;     const int c = lane & 7;
; #pragma unroll
;     for (int j = 0; j < 4; ++j) { const int n = (lane >> 3) + 8 * j; const LAS float* s = scr + (8 * c) * 33 + n;
;         const unsigned long long o = (unsigned long long)pg8::pk4_fp8(s[0 * 33], s[1 * 33], s[2 * 33], s[3 * 33]) | ((unsigned long long)pg8::pk4_fp8(s[4 * 33], s[5 * 33], s[6 * 33], s[7 * 33]) << 32);
;         *(GAS unsigned long long*)(WT + (size_t)(n0 + n) * K + k0 + 8 * c) = o; }
;     LDS_WAIT(); asm volatile("" ::: "memory");
	s_add_u32 s8, s34, 0x2000
	s_addc_u32 s9, s35, 0
	global_load_dwordx4 v[144:147], v74, s[8:9]
	s_add_u32 s8, s8, 0x20000
	s_addc_u32 s9, s9, 0
	global_load_dwordx4 v[148:151], v74, s[8:9]
	s_add_u32 s8, s8, 0x20000
	s_addc_u32 s9, s9, 0
	global_load_dwordx4 v[152:155], v74, s[8:9]
	s_add_u32 s8, s8, 0x20000
	s_addc_u32 s9, s9, 0
	global_load_dwordx4 v[156:159], v74, s[8:9]
	s_add_u32 s8, s8, 0x20000
	s_addc_u32 s9, s9, 0
	global_load_dwordx4 v[160:163], v74, s[8:9]
	s_add_u32 s8, s8, 0x20000
	s_addc_u32 s9, s9, 0
	global_load_dwordx4 v[164:167], v74, s[8:9]
	s_add_u32 s8, s8, 0x20000
	s_addc_u32 s9, s9, 0
	global_load_dwordx4 v[168:171], v74, s[8:9]
	s_add_u32 s8, s8, 0x20000
	s_addc_u32 s9, s9, 0
	global_load_dwordx4 v[172:175], v74, s[8:9]
	s_mov_b64 s[6:7], s[36:37]
	ds_read_b32 v226, v211
	ds_read_b32 v227, v211 offset:512
	ds_read_b32 v228, v211 offset:1024
	ds_read_b32 v229, v211 offset:1536
	ds_read_b32 v230, v211 offset:2048
	ds_read_b32 v231, v211 offset:2560
	ds_read_b32 v232, v211 offset:3072
	ds_read_b32 v233, v211 offset:3584
	ds_read_b32 v234, v211 offset:4096
	ds_read_b32 v235, v211 offset:4608
	ds_read_b32 v236, v211 offset:5120
	ds_read_b32 v237, v211 offset:5632
	ds_read_b32 v238, v211 offset:6144
	ds_read_b32 v239, v211 offset:6656
	ds_read_b32 v240, v211 offset:7168
	ds_read_b32 v241, v211 offset:7680
	s_waitcnt lgkmcnt(0)
	v_max_f32_e32 v226, v226, v226
	v_max_f32_e32 v227, v227, v227
	v_max_f32_e32 v228, v228, v228
	v_max_f32_e32 v229, v229, v229
	v_max_f32_e32 v230, v230, v230
	v_max_f32_e32 v231, v231, v231
	v_max_f32_e32 v232, v232, v232
	v_max_f32_e32 v233, v233, v233
	v_max_f32_e32 v234, v234, v234
	v_max_f32_e32 v235, v235, v235
	v_max_f32_e32 v236, v236, v236
	v_max_f32_e32 v237, v237, v237
	v_max_f32_e32 v238, v238, v238
	v_max_f32_e32 v239, v239, v239
	v_max_f32_e32 v240, v240, v240
	v_max_f32_e32 v241, v241, v241
	v_med3_f32 v226, v226, s62, v95
	v_med3_f32 v227, v227, s62, v95
	v_med3_f32 v228, v228, s62, v95
	v_med3_f32 v229, v229, s62, v95
	v_med3_f32 v230, v230, s62, v95
	v_med3_f32 v231, v231, s62, v95
	v_med3_f32 v232, v232, s62, v95
	v_med3_f32 v233, v233, s62, v95
	v_med3_f32 v234, v234, s62, v95
	v_med3_f32 v235, v235, s62, v95
	v_med3_f32 v236, v236, s62, v95
	v_med3_f32 v237, v237, s62, v95
	v_med3_f32 v238, v238, s62, v95
	v_med3_f32 v239, v239, s62, v95
	v_med3_f32 v240, v240, s62, v95
	v_med3_f32 v241, v241, s62, v95
	v_mov_b32_e32 v242, 0
	v_mov_b32_e32 v243, 0
	v_mov_b32_e32 v244, 0
	v_mov_b32_e32 v245, 0
	v_cvt_pk_fp8_f32 v242, v226, v227
	v_cvt_pk_fp8_f32 v243, v230, v231
	v_cvt_pk_fp8_f32 v244, v234, v235
	v_cvt_pk_fp8_f32 v245, v238, v239
	v_cvt_pk_fp8_f32 v242, v228, v229 op_sel:[0,0,1]
	v_cvt_pk_fp8_f32 v243, v232, v233 op_sel:[0,0,1]
	v_cvt_pk_fp8_f32 v244, v236, v237 op_sel:[0,0,1]
	v_cvt_pk_fp8_f32 v245, v240, v241 op_sel:[0,0,1]
	s_nop 0
	global_store_dwordx4 v77, v[242:245], s[6:7]
	ds_read_b32 v226, v213
	ds_read_b32 v227, v213 offset:512
	ds_read_b32 v228, v213 offset:1024
	ds_read_b32 v229, v213 offset:1536
	ds_read_b32 v230, v213 offset:2048
	ds_read_b32 v231, v213 offset:2560
	ds_read_b32 v232, v213 offset:3072
	ds_read_b32 v233, v213 offset:3584
	ds_read_b32 v234, v213 offset:4096
	ds_read_b32 v235, v213 offset:4608
	ds_read_b32 v236, v213 offset:5120
	ds_read_b32 v237, v213 offset:5632
	ds_read_b32 v238, v213 offset:6144
	ds_read_b32 v239, v213 offset:6656
	ds_read_b32 v240, v213 offset:7168
	ds_read_b32 v241, v213 offset:7680
	s_waitcnt lgkmcnt(0)
	v_max_f32_e32 v226, v226, v226
	v_max_f32_e32 v227, v227, v227
	v_max_f32_e32 v228, v228, v228
	v_max_f32_e32 v229, v229, v229
	v_max_f32_e32 v230, v230, v230
	v_max_f32_e32 v231, v231, v231
	v_max_f32_e32 v232, v232, v232
	v_max_f32_e32 v233, v233, v233
	v_max_f32_e32 v234, v234, v234
	v_max_f32_e32 v235, v235, v235
	v_max_f32_e32 v236, v236, v236
	v_max_f32_e32 v237, v237, v237
	v_max_f32_e32 v238, v238, v238
	v_max_f32_e32 v239, v239, v239
	v_max_f32_e32 v240, v240, v240
	v_max_f32_e32 v241, v241, v241
	v_med3_f32 v226, v226, s62, v95
	v_med3_f32 v227, v227, s62, v95
	v_med3_f32 v228, v228, s62, v95
	v_med3_f32 v229, v229, s62, v95
	v_med3_f32 v230, v230, s62, v95
	v_med3_f32 v231, v231, s62, v95
	v_med3_f32 v232, v232, s62, v95
	v_med3_f32 v233, v233, s62, v95
	v_med3_f32 v234, v234, s62, v95
	v_med3_f32 v235, v235, s62, v95
	v_med3_f32 v236, v236, s62, v95
	v_med3_f32 v237, v237, s62, v95
	v_med3_f32 v238, v238, s62, v95
	v_med3_f32 v239, v239, s62, v95
	v_med3_f32 v240, v240, s62, v95
	v_med3_f32 v241, v241, s62, v95
	v_mov_b32_e32 v242, 0
	v_mov_b32_e32 v243, 0
	v_mov_b32_e32 v244, 0
	v_mov_b32_e32 v245, 0
	v_cvt_pk_fp8_f32 v242, v226, v227
	v_cvt_pk_fp8_f32 v243, v230, v231
	v_cvt_pk_fp8_f32 v244, v234, v235
	v_cvt_pk_fp8_f32 v245, v238, v239
	v_cvt_pk_fp8_f32 v242, v228, v229 op_sel:[0,0,1]
	v_cvt_pk_fp8_f32 v243, v232, v233 op_sel:[0,0,1]
	v_cvt_pk_fp8_f32 v244, v236, v237 op_sel:[0,0,1]
	v_cvt_pk_fp8_f32 v245, v240, v241 op_sel:[0,0,1]
	s_nop 0
	global_store_dwordx4 v78, v[242:245], s[6:7]
	s_waitcnt vmcnt(12)
	v_mul_f32_e32 v176, v34, v176
	v_mul_f32_e32 v177, v34, v177
	v_mul_f32_e32 v178, v34, v178
	v_mul_f32_e32 v179, v34, v179
	ds_write_b128 v210, v[176:179]
	v_mul_f32_e32 v180, v35, v180
	v_mul_f32_e32 v181, v35, v181
	v_mul_f32_e32 v182, v35, v182
	v_mul_f32_e32 v183, v35, v183
	ds_write_b128 v210, v[180:183] offset:1024
	v_mul_f32_e32 v184, v36, v184
	v_mul_f32_e32 v185, v36, v185
	v_mul_f32_e32 v186, v36, v186
	v_mul_f32_e32 v187, v36, v187
	ds_write_b128 v210, v[184:187] offset:2048
	v_mul_f32_e32 v188, v37, v188
	v_mul_f32_e32 v189, v37, v189
	v_mul_f32_e32 v190, v37, v190
	v_mul_f32_e32 v191, v37, v191
	ds_write_b128 v210, v[188:191] offset:3072
	v_mul_f32_e32 v192, v38, v192
	v_mul_f32_e32 v193, v38, v193
	v_mul_f32_e32 v194, v38, v194
	v_mul_f32_e32 v195, v38, v195
	ds_write_b128 v210, v[192:195] offset:4096
	v_mul_f32_e32 v196, v39, v196
	v_mul_f32_e32 v197, v39, v197
	v_mul_f32_e32 v198, v39, v198
	v_mul_f32_e32 v199, v39, v199
	ds_write_b128 v210, v[196:199] offset:5120
	v_mul_f32_e32 v200, v40, v200
	v_mul_f32_e32 v201, v40, v201
	v_mul_f32_e32 v202, v40, v202
	v_mul_f32_e32 v203, v40, v203
	ds_write_b128 v210, v[200:203] offset:6144
	v_mul_f32_e32 v204, v41, v204
	v_mul_f32_e32 v205, v41, v205
	v_mul_f32_e32 v206, v41, v206
	v_mul_f32_e32 v207, v41, v207
	ds_write_b128 v210, v[204:207] offset:7168
	s_waitcnt lgkmcnt(0)
	s_barrier
; #define GAS __attribute__((address_space(1)))
; #define LAS __attribute__((address_space(3)))
; #define LDS_WAIT() asm volatile("s_waitcnt lgkmcnt(0)" ::: "memory")
; __device__ __forceinline__ unsigned pk4_fp8(float a, float b, float c, float d) {
;     a = fminf(fmaxf(a, -448.f), 448.f); b = fminf(fmaxf(b, -448.f), 448.f); c = fminf(fmaxf(c, -448.f), 448.f); d = fminf(fmaxf(d, -448.f), 448.f);
;     int w = __builtin_amdgcn_cvt_pk_fp8_f32(a, b, 0, false); w = __builtin_amdgcn_cvt_pk_fp8_f32(c, d, w, true); return (unsigned)w; }
;     const int pr = item >> 1, kb = 2 * (pr / nblk) + (item & 1), nb = pr % nblk, k0 = 64 * kb, n0 = 32 * nb;
;     const int nr = n0 + (lane & 31); const int sc = MAP == 1 ? src_col_in(nr) : nr;
;     float v[32];
; #pragma unroll
;     for (int i = 0; i < 32; ++i) v[i] = sc >= 0 ? W[(size_t)(k0 + 2 * i + (lane >> 5)) * Nsrc + sc] : 0.f;
; #pragma unroll
;     for (int i = 0; i < 32; ++i) { const int k = k0 + 2 * i + (lane >> 5); float x = v[i] * wscale; if (KS) x *= (k < ksplit ? ksA[k] : ksB[k - ksplit]); scr[(2 * i + (lane >> 5)) * 33 + (lane & 31)] = x; }
;     LDS_WAIT(); asm volatile("" ::: "memory");
;     const int c = lane & 7;
; #pragma unroll
;     for (int j = 0; j < 4; ++j) { const int n = (lane >> 3) + 8 * j; const LAS float* s = scr + (8 * c) * 33 + n;
;         const unsigned long long o = (unsigned long long)pg8::pk4_fp8(s[0 * 33], s[1 * 33], s[2 * 33], s[3 * 33]) | ((unsigned long long)pg8::pk4_fp8(s[4 * 33], s[5 * 33], s[6 * 33], s[7 * 33]) << 32);
;         *(GAS unsigned long long*)(WT + (size_t)(n0 + n) * K + k0 + 8 * c) = o; }
;     LDS_WAIT(); asm volatile("" ::: "memory");
	s_add_u32 s8, s34, 0x3000
	s_addc_u32 s9, s35, 0
	global_load_dwordx4 v[176:179], v74, s[8:9]
	s_add_u32 s8, s8, 0x20000
	s_addc_u32 s9, s9, 0
	global_load_dwordx4 v[180:183], v74, s[8:9]
	s_add_u32 s8, s8, 0x20000
	s_addc_u32 s9, s9, 0
	global_load_dwordx4 v[184:187], v74, s[8:9]
	s_add_u32 s8, s8, 0x20000
	s_addc_u32 s9, s9, 0
	global_load_dwordx4 v[188:191], v74, s[8:9]
	s_add_u32 s8, s8, 0x20000
	s_addc_u32 s9, s9, 0
	global_load_dwordx4 v[192:195], v74, s[8:9]
	s_add_u32 s8, s8, 0x20000
	s_addc_u32 s9, s9, 0
	global_load_dwordx4 v[196:199], v74, s[8:9]
	s_add_u32 s8, s8, 0x20000
	s_addc_u32 s9, s9, 0
	global_load_dwordx4 v[200:203], v74, s[8:9]
	s_add_u32 s8, s8, 0x20000
	s_addc_u32 s9, s9, 0
	global_load_dwordx4 v[204:207], v74, s[8:9]
	s_add_u32 s6, s36, 0x400000
	s_addc_u32 s7, s37, 0
	ds_read_b32 v226, v212
	ds_read_b32 v227, v212 offset:512
	ds_read_b32 v228, v212 offset:1024
	ds_read_b32 v229, v212 offset:1536
	ds_read_b32 v230, v212 offset:2048
	ds_read_b32 v231, v212 offset:2560
	ds_read_b32 v232, v212 offset:3072
	ds_read_b32 v233, v212 offset:3584
	ds_read_b32 v234, v212 offset:4096
	ds_read_b32 v235, v212 offset:4608
	ds_read_b32 v236, v212 offset:5120
	ds_read_b32 v237, v212 offset:5632
	ds_read_b32 v238, v212 offset:6144
	ds_read_b32 v239, v212 offset:6656
	ds_read_b32 v240, v212 offset:7168
	ds_read_b32 v241, v212 offset:7680
	s_waitcnt lgkmcnt(0)
	v_max_f32_e32 v226, v226, v226
	v_max_f32_e32 v227, v227, v227
	v_max_f32_e32 v228, v228, v228
	v_max_f32_e32 v229, v229, v229
	v_max_f32_e32 v230, v230, v230
	v_max_f32_e32 v231, v231, v231
	v_max_f32_e32 v232, v232, v232
	v_max_f32_e32 v233, v233, v233
	v_max_f32_e32 v234, v234, v234
	v_max_f32_e32 v235, v235, v235
	v_max_f32_e32 v236, v236, v236
	v_max_f32_e32 v237, v237, v237
	v_max_f32_e32 v238, v238, v238
	v_max_f32_e32 v239, v239, v239
	v_max_f32_e32 v240, v240, v240
	v_max_f32_e32 v241, v241, v241
	v_med3_f32 v226, v226, s62, v95
	v_med3_f32 v227, v227, s62, v95
	v_med3_f32 v228, v228, s62, v95
	v_med3_f32 v229, v229, s62, v95
	v_med3_f32 v230, v230, s62, v95
	v_med3_f32 v231, v231, s62, v95
	v_med3_f32 v232, v232, s62, v95
	v_med3_f32 v233, v233, s62, v95
	v_med3_f32 v234, v234, s62, v95
	v_med3_f32 v235, v235, s62, v95
	v_med3_f32 v236, v236, s62, v95
	v_med3_f32 v237, v237, s62, v95
	v_med3_f32 v238, v238, s62, v95
	v_med3_f32 v239, v239, s62, v95
	v_med3_f32 v240, v240, s62, v95
	v_med3_f32 v241, v241, s62, v95
	v_mov_b32_e32 v242, 0
	v_mov_b32_e32 v243, 0
	v_mov_b32_e32 v244, 0
	v_mov_b32_e32 v245, 0
	v_cvt_pk_fp8_f32 v242, v226, v227
	v_cvt_pk_fp8_f32 v243, v230, v231
	v_cvt_pk_fp8_f32 v244, v234, v235
	v_cvt_pk_fp8_f32 v245, v238, v239
	v_cvt_pk_fp8_f32 v242, v228, v229 op_sel:[0,0,1]
	v_cvt_pk_fp8_f32 v243, v232, v233 op_sel:[0,0,1]
	v_cvt_pk_fp8_f32 v244, v236, v237 op_sel:[0,0,1]
	v_cvt_pk_fp8_f32 v245, v240, v241 op_sel:[0,0,1]
	s_nop 0
	global_store_dwordx4 v77, v[242:245], s[6:7]
	ds_read_b32 v226, v214
	ds_read_b32 v227, v214 offset:512
	ds_read_b32 v228, v214 offset:1024
	ds_read_b32 v229, v214 offset:1536
	ds_read_b32 v230, v214 offset:2048
	ds_read_b32 v231, v214 offset:2560
	ds_read_b32 v232, v214 offset:3072
	ds_read_b32 v233, v214 offset:3584
	ds_read_b32 v234, v214 offset:4096
	ds_read_b32 v235, v214 offset:4608
	ds_read_b32 v236, v214 offset:5120
	ds_read_b32 v237, v214 offset:5632
	ds_read_b32 v238, v214 offset:6144
	ds_read_b32 v239, v214 offset:6656
	ds_read_b32 v240, v214 offset:7168
	ds_read_b32 v241, v214 offset:7680
	s_waitcnt lgkmcnt(0)
	v_max_f32_e32 v226, v226, v226
	v_max_f32_e32 v227, v227, v227
	v_max_f32_e32 v228, v228, v228
	v_max_f32_e32 v229, v229, v229
	v_max_f32_e32 v230, v230, v230
	v_max_f32_e32 v231, v231, v231
	v_max_f32_e32 v232, v232, v232
	v_max_f32_e32 v233, v233, v233
	v_max_f32_e32 v234, v234, v234
	v_max_f32_e32 v235, v235, v235
	v_max_f32_e32 v236, v236, v236
	v_max_f32_e32 v237, v237, v237
	v_max_f32_e32 v238, v238, v238
	v_max_f32_e32 v239, v239, v239
	v_max_f32_e32 v240, v240, v240
	v_max_f32_e32 v241, v241, v241
	v_med3_f32 v226, v226, s62, v95
	v_med3_f32 v227, v227, s62, v95
	v_med3_f32 v228, v228, s62, v95
	v_med3_f32 v229, v229, s62, v95
	v_med3_f32 v230, v230, s62, v95
	v_med3_f32 v231, v231, s62, v95
	v_med3_f32 v232, v232, s62, v95
	v_med3_f32 v233, v233, s62, v95
	v_med3_f32 v234, v234, s62, v95
	v_med3_f32 v235, v235, s62, v95
	v_med3_f32 v236, v236, s62, v95
	v_med3_f32 v237, v237, s62, v95
	v_med3_f32 v238, v238, s62, v95
	v_med3_f32 v239, v239, s62, v95
	v_med3_f32 v240, v240, s62, v95
	v_med3_f32 v241, v241, s62, v95
	v_mov_b32_e32 v242, 0
	v_mov_b32_e32 v243, 0
	v_mov_b32_e32 v244, 0
	v_mov_b32_e32 v245, 0
	v_cvt_pk_fp8_f32 v242, v226, v227
	v_cvt_pk_fp8_f32 v243, v230, v231
	v_cvt_pk_fp8_f32 v244, v234, v235
	v_cvt_pk_fp8_f32 v245, v238, v239
	v_cvt_pk_fp8_f32 v242, v228, v229 op_sel:[0,0,1]
	v_cvt_pk_fp8_f32 v243, v232, v233 op_sel:[0,0,1]
	v_cvt_pk_fp8_f32 v244, v236, v237 op_sel:[0,0,1]
	v_cvt_pk_fp8_f32 v245, v240, v241 op_sel:[0,0,1]
	s_nop 0
	global_store_dwordx4 v78, v[242:245], s[6:7]
	s_waitcnt vmcnt(12)
	v_mul_f32_e32 v144, v34, v144
	v_mul_f32_e32 v145, v34, v145
	v_mul_f32_e32 v146, v34, v146
	v_mul_f32_e32 v147, v34, v147
	ds_write_b128 v209, v[144:147]
	v_mul_f32_e32 v148, v35, v148
	v_mul_f32_e32 v149, v35, v149
	v_mul_f32_e32 v150, v35, v150
	v_mul_f32_e32 v151, v35, v151
	ds_write_b128 v209, v[148:151] offset:1024
	v_mul_f32_e32 v152, v36, v152
	v_mul_f32_e32 v153, v36, v153
	v_mul_f32_e32 v154, v36, v154
	v_mul_f32_e32 v155, v36, v155
	ds_write_b128 v209, v[152:155] offset:2048
	v_mul_f32_e32 v156, v37, v156
	v_mul_f32_e32 v157, v37, v157
	v_mul_f32_e32 v158, v37, v158
	v_mul_f32_e32 v159, v37, v159
	ds_write_b128 v209, v[156:159] offset:3072
	v_mul_f32_e32 v160, v38, v160
	v_mul_f32_e32 v161, v38, v161
	v_mul_f32_e32 v162, v38, v162
	v_mul_f32_e32 v163, v38, v163
	ds_write_b128 v209, v[160:163] offset:4096
	v_mul_f32_e32 v164, v39, v164
	v_mul_f32_e32 v165, v39, v165
	v_mul_f32_e32 v166, v39, v166
	v_mul_f32_e32 v167, v39, v167
	ds_write_b128 v209, v[164:167] offset:5120
	v_mul_f32_e32 v168, v40, v168
	v_mul_f32_e32 v169, v40, v169
	v_mul_f32_e32 v170, v40, v170
	v_mul_f32_e32 v171, v40, v171
	ds_write_b128 v209, v[168:171] offset:6144
	v_mul_f32_e32 v172, v41, v172
	v_mul_f32_e32 v173, v41, v173
	v_mul_f32_e32 v174, v41, v174
	v_mul_f32_e32 v175, v41, v175
	ds_write_b128 v209, v[172:175] offset:7168
	s_waitcnt lgkmcnt(0)
	s_barrier
; #define GAS __attribute__((address_space(1)))
; #define LAS __attribute__((address_space(3)))
; #define LDS_WAIT() asm volatile("s_waitcnt lgkmcnt(0)" ::: "memory")
; __device__ __forceinline__ unsigned pk4_fp8(float a, float b, float c, float d) {
;     a = fminf(fmaxf(a, -448.f), 448.f); b = fminf(fmaxf(b, -448.f), 448.f); c = fminf(fmaxf(c, -448.f), 448.f); d = fminf(fmaxf(d, -448.f), 448.f);
;     int w = __builtin_amdgcn_cvt_pk_fp8_f32(a, b, 0, false); w = __builtin_amdgcn_cvt_pk_fp8_f32(c, d, w, true); return (unsigned)w; }
;     const int pr = item >> 1, kb = 2 * (pr / nblk) + (item & 1), nb = pr % nblk, k0 = 64 * kb, n0 = 32 * nb;
;     const int nr = n0 + (lane & 31); const int sc = MAP == 1 ? src_col_in(nr) : nr;
;     float v[32];
; #pragma unroll
;     for (int i = 0; i < 32; ++i) v[i] = sc >= 0 ? W[(size_t)(k0 + 2 * i + (lane >> 5)) * Nsrc + sc] : 0.f;
; #pragma unroll
;     for (int i = 0; i < 32; ++i) { const int k = k0 + 2 * i + (lane >> 5); float x = v[i] * wscale; if (KS) x *= (k < ksplit ? ksA[k] : ksB[k - ksplit]); scr[(2 * i + (lane >> 5)) * 33 + (lane & 31)] = x; }
;     LDS_WAIT(); asm volatile("" ::: "memory");
;     const int c = lane & 7;
; #pragma unroll
;     for (int j = 0; j < 4; ++j) { const int n = (lane >> 3) + 8 * j; const LAS float* s = scr + (8 * c) * 33 + n;
;         const unsigned long long o = (unsigned long long)pg8::pk4_fp8(s[0 * 33], s[1 * 33], s[2 * 33], s[3 * 33]) | ((unsigned long long)pg8::pk4_fp8(s[4 * 33], s[5 * 33], s[6 * 33], s[7 * 33]) << 32);
;         *(GAS unsigned long long*)(WT + (size_t)(n0 + n) * K + k0 + 8 * c) = o; }
;     LDS_WAIT(); asm volatile("" ::: "memory");
	s_add_u32 s8, s34, 0x4000
	s_addc_u32 s9, s35, 0
	global_load_dwordx4 v[144:147], v74, s[8:9]
	s_add_u32 s8, s8, 0x20000
	s_addc_u32 s9, s9, 0
	global_load_dwordx4 v[148:151], v74, s[8:9]
	s_add_u32 s8, s8, 0x20000
	s_addc_u32 s9, s9, 0
	global_load_dwordx4 v[152:155], v74, s[8:9]
	s_add_u32 s8, s8, 0x20000
	s_addc_u32 s9, s9, 0
	global_load_dwordx4 v[156:159], v74, s[8:9]
	s_add_u32 s8, s8, 0x20000
	s_addc_u32 s9, s9, 0
	global_load_dwordx4 v[160:163], v74, s[8:9]
	s_add_u32 s8, s8, 0x20000
	s_addc_u32 s9, s9, 0
	global_load_dwordx4 v[164:167], v74, s[8:9]
	s_add_u32 s8, s8, 0x20000
	s_addc_u32 s9, s9, 0
	global_load_dwordx4 v[168:171], v74, s[8:9]
	s_add_u32 s8, s8, 0x20000
	s_addc_u32 s9, s9, 0
	global_load_dwordx4 v[172:175], v74, s[8:9]
	s_add_u32 s6, s36, 0x800000
	s_addc_u32 s7, s37, 0
	ds_read_b32 v226, v211
	ds_read_b32 v227, v211 offset:512
	ds_read_b32 v228, v211 offset:1024
	ds_read_b32 v229, v211 offset:1536
	ds_read_b32 v230, v211 offset:2048
	ds_read_b32 v231, v211 offset:2560
	ds_read_b32 v232, v211 offset:3072
	ds_read_b32 v233, v211 offset:3584
	ds_read_b32 v234, v211 offset:4096
	ds_read_b32 v235, v211 offset:4608
	ds_read_b32 v236, v211 offset:5120
	ds_read_b32 v237, v211 offset:5632
	ds_read_b32 v238, v211 offset:6144
	ds_read_b32 v239, v211 offset:6656
	ds_read_b32 v240, v211 offset:7168
	ds_read_b32 v241, v211 offset:7680
	s_waitcnt lgkmcnt(0)
	v_max_f32_e32 v226, v226, v226
	v_max_f32_e32 v227, v227, v227
	v_max_f32_e32 v228, v228, v228
	v_max_f32_e32 v229, v229, v229
	v_max_f32_e32 v230, v230, v230
	v_max_f32_e32 v231, v231, v231
	v_max_f32_e32 v232, v232, v232
	v_max_f32_e32 v233, v233, v233
	v_max_f32_e32 v234, v234, v234
	v_max_f32_e32 v235, v235, v235
	v_max_f32_e32 v236, v236, v236
	v_max_f32_e32 v237, v237, v237
	v_max_f32_e32 v238, v238, v238
	v_max_f32_e32 v239, v239, v239
	v_max_f32_e32 v240, v240, v240
	v_max_f32_e32 v241, v241, v241
	v_med3_f32 v226, v226, s62, v95
	v_med3_f32 v227, v227, s62, v95
	v_med3_f32 v228, v228, s62, v95
	v_med3_f32 v229, v229, s62, v95
	v_med3_f32 v230, v230, s62, v95
	v_med3_f32 v231, v231, s62, v95
	v_med3_f32 v232, v232, s62, v95
	v_med3_f32 v233, v233, s62, v95
	v_med3_f32 v234, v234, s62, v95
	v_med3_f32 v235, v235, s62, v95
	v_med3_f32 v236, v236, s62, v95
	v_med3_f32 v237, v237, s62, v95
	v_med3_f32 v238, v238, s62, v95
	v_med3_f32 v239, v239, s62, v95
	v_med3_f32 v240, v240, s62, v95
	v_med3_f32 v241, v241, s62, v95
	v_mov_b32_e32 v242, 0
	v_mov_b32_e32 v243, 0
	v_mov_b32_e32 v244, 0
	v_mov_b32_e32 v245, 0
	v_cvt_pk_fp8_f32 v242, v226, v227
	v_cvt_pk_fp8_f32 v243, v230, v231
	v_cvt_pk_fp8_f32 v244, v234, v235
	v_cvt_pk_fp8_f32 v245, v238, v239
	v_cvt_pk_fp8_f32 v242, v228, v229 op_sel:[0,0,1]
	v_cvt_pk_fp8_f32 v243, v232, v233 op_sel:[0,0,1]
	v_cvt_pk_fp8_f32 v244, v236, v237 op_sel:[0,0,1]
	v_cvt_pk_fp8_f32 v245, v240, v241 op_sel:[0,0,1]
	s_nop 0
	global_store_dwordx4 v77, v[242:245], s[6:7]
	ds_read_b32 v226, v213
	ds_read_b32 v227, v213 offset:512
	ds_read_b32 v228, v213 offset:1024
	ds_read_b32 v229, v213 offset:1536
	ds_read_b32 v230, v213 offset:2048
	ds_read_b32 v231, v213 offset:2560
	ds_read_b32 v232, v213 offset:3072
	ds_read_b32 v233, v213 offset:3584
	ds_read_b32 v234, v213 offset:4096
	ds_read_b32 v235, v213 offset:4608
	ds_read_b32 v236, v213 offset:5120
	ds_read_b32 v237, v213 offset:5632
	ds_read_b32 v238, v213 offset:6144
	ds_read_b32 v239, v213 offset:6656
	ds_read_b32 v240, v213 offset:7168
	ds_read_b32 v241, v213 offset:7680
	s_waitcnt lgkmcnt(0)
	v_max_f32_e32 v226, v226, v226
	v_max_f32_e32 v227, v227, v227
	v_max_f32_e32 v228, v228, v228
	v_max_f32_e32 v229, v229, v229
	v_max_f32_e32 v230, v230, v230
	v_max_f32_e32 v231, v231, v231
	v_max_f32_e32 v232, v232, v232
	v_max_f32_e32 v233, v233, v233
	v_max_f32_e32 v234, v234, v234
	v_max_f32_e32 v235, v235, v235
	v_max_f32_e32 v236, v236, v236
	v_max_f32_e32 v237, v237, v237
	v_max_f32_e32 v238, v238, v238
	v_max_f32_e32 v239, v239, v239
	v_max_f32_e32 v240, v240, v240
	v_max_f32_e32 v241, v241, v241
	v_med3_f32 v226, v226, s62, v95
	v_med3_f32 v227, v227, s62, v95
	v_med3_f32 v228, v228, s62, v95
	v_med3_f32 v229, v229, s62, v95
	v_med3_f32 v230, v230, s62, v95
	v_med3_f32 v231, v231, s62, v95
	v_med3_f32 v232, v232, s62, v95
	v_med3_f32 v233, v233, s62, v95
	v_med3_f32 v234, v234, s62, v95
	v_med3_f32 v235, v235, s62, v95
	v_med3_f32 v236, v236, s62, v95
	v_med3_f32 v237, v237, s62, v95
	v_med3_f32 v238, v238, s62, v95
	v_med3_f32 v239, v239, s62, v95
	v_med3_f32 v240, v240, s62, v95
	v_med3_f32 v241, v241, s62, v95
	v_mov_b32_e32 v242, 0
	v_mov_b32_e32 v243, 0
	v_mov_b32_e32 v244, 0
	v_mov_b32_e32 v245, 0
	v_cvt_pk_fp8_f32 v242, v226, v227
	v_cvt_pk_fp8_f32 v243, v230, v231
	v_cvt_pk_fp8_f32 v244, v234, v235
	v_cvt_pk_fp8_f32 v245, v238, v239
	v_cvt_pk_fp8_f32 v242, v228, v229 op_sel:[0,0,1]
	v_cvt_pk_fp8_f32 v243, v232, v233 op_sel:[0,0,1]
	v_cvt_pk_fp8_f32 v244, v236, v237 op_sel:[0,0,1]
	v_cvt_pk_fp8_f32 v245, v240, v241 op_sel:[0,0,1]
	s_nop 0
	global_store_dwordx4 v78, v[242:245], s[6:7]
	s_waitcnt vmcnt(12)
	v_mul_f32_e32 v176, v34, v176
	v_mul_f32_e32 v177, v34, v177
	v_mul_f32_e32 v178, v34, v178
	v_mul_f32_e32 v179, v34, v179
	ds_write_b128 v210, v[176:179]
	v_mul_f32_e32 v180, v35, v180
	v_mul_f32_e32 v181, v35, v181
	v_mul_f32_e32 v182, v35, v182
	v_mul_f32_e32 v183, v35, v183
	ds_write_b128 v210, v[180:183] offset:1024
	v_mul_f32_e32 v184, v36, v184
	v_mul_f32_e32 v185, v36, v185
	v_mul_f32_e32 v186, v36, v186
	v_mul_f32_e32 v187, v36, v187
	ds_write_b128 v210, v[184:187] offset:2048
	v_mul_f32_e32 v188, v37, v188
	v_mul_f32_e32 v189, v37, v189
	v_mul_f32_e32 v190, v37, v190
	v_mul_f32_e32 v191, v37, v191
	ds_write_b128 v210, v[188:191] offset:3072
	v_mul_f32_e32 v192, v38, v192
	v_mul_f32_e32 v193, v38, v193
	v_mul_f32_e32 v194, v38, v194
	v_mul_f32_e32 v195, v38, v195
	ds_write_b128 v210, v[192:195] offset:4096
	v_mul_f32_e32 v196, v39, v196
	v_mul_f32_e32 v197, v39, v197
	v_mul_f32_e32 v198, v39, v198
	v_mul_f32_e32 v199, v39, v199
	ds_write_b128 v210, v[196:199] offset:5120
	v_mul_f32_e32 v200, v40, v200
	v_mul_f32_e32 v201, v40, v201
	v_mul_f32_e32 v202, v40, v202
	v_mul_f32_e32 v203, v40, v203
	ds_write_b128 v210, v[200:203] offset:6144
	v_mul_f32_e32 v204, v41, v204
	v_mul_f32_e32 v205, v41, v205
	v_mul_f32_e32 v206, v41, v206
	v_mul_f32_e32 v207, v41, v207
	ds_write_b128 v210, v[204:207] offset:7168
	s_waitcnt lgkmcnt(0)
	s_barrier
; #define GAS __attribute__((address_space(1)))
; #define LAS __attribute__((address_space(3)))
; #define LDS_WAIT() asm volatile("s_waitcnt lgkmcnt(0)" ::: "memory")
; __device__ __forceinline__ unsigned pk4_fp8(float a, float b, float c, float d) {
;     a = fminf(fmaxf(a, -448.f), 448.f); b = fminf(fmaxf(b, -448.f), 448.f); c = fminf(fmaxf(c, -448.f), 448.f); d = fminf(fmaxf(d, -448.f), 448.f);
;     int w = __builtin_amdgcn_cvt_pk_fp8_f32(a, b, 0, false); w = __builtin_amdgcn_cvt_pk_fp8_f32(c, d, w, true); return (unsigned)w; }
;     const int pr = item >> 1, kb = 2 * (pr / nblk) + (item & 1), nb = pr % nblk, k0 = 64 * kb, n0 = 32 * nb;
;     const int nr = n0 + (lane & 31); const int sc = MAP == 1 ? src_col_in(nr) : nr;
;     float v[32];
; #pragma unroll
;     for (int i = 0; i < 32; ++i) v[i] = sc >= 0 ? W[(size_t)(k0 + 2 * i + (lane >> 5)) * Nsrc + sc] : 0.f;
; #pragma unroll
;     for (int i = 0; i < 32; ++i) { const int k = k0 + 2 * i + (lane >> 5); float x = v[i] * wscale; if (KS) x *= (k < ksplit ? ksA[k] : ksB[k - ksplit]); scr[(2 * i + (lane >> 5)) * 33 + (lane & 31)] = x; }
;     LDS_WAIT(); asm volatile("" ::: "memory");
;     const int c = lane & 7;
; #pragma unroll
;     for (int j = 0; j < 4; ++j) { const int n = (lane >> 3) + 8 * j; const LAS float* s = scr + (8 * c) * 33 + n;
;         const unsigned long long o = (unsigned long long)pg8::pk4_fp8(s[0 * 33], s[1 * 33], s[2 * 33], s[3 * 33]) | ((unsigned long long)pg8::pk4_fp8(s[4 * 33], s[5 * 33], s[6 * 33], s[7 * 33]) << 32);
;         *(GAS unsigned long long*)(WT + (size_t)(n0 + n) * K + k0 + 8 * c) = o; }
;     LDS_WAIT(); asm volatile("" ::: "memory");
	s_add_u32 s8, s34, 0x5000
	s_addc_u32 s9, s35, 0
	global_load_dwordx4 v[176:179], v74, s[8:9]
	s_add_u32 s8, s8, 0x20000
	s_addc_u32 s9, s9, 0
	global_load_dwordx4 v[180:183], v74, s[8:9]
	s_add_u32 s8, s8, 0x20000
	s_addc_u32 s9, s9, 0
	global_load_dwordx4 v[184:187], v74, s[8:9]
	s_add_u32 s8, s8, 0x20000
	s_addc_u32 s9, s9, 0
	global_load_dwordx4 v[188:191], v74, s[8:9]
	s_add_u32 s8, s8, 0x20000
	s_addc_u32 s9, s9, 0
	global_load_dwordx4 v[192:195], v74, s[8:9]
	s_add_u32 s8, s8, 0x20000
	s_addc_u32 s9, s9, 0
	global_load_dwordx4 v[196:199], v74, s[8:9]
	s_add_u32 s8, s8, 0x20000
	s_addc_u32 s9, s9, 0
	global_load_dwordx4 v[200:203], v74, s[8:9]
	s_add_u32 s8, s8, 0x20000
	s_addc_u32 s9, s9, 0
	global_load_dwordx4 v[204:207], v74, s[8:9]
	s_add_u32 s6, s36, 0xc00000
	s_addc_u32 s7, s37, 0
	ds_read_b32 v226, v212
	ds_read_b32 v227, v212 offset:512
	ds_read_b32 v228, v212 offset:1024
	ds_read_b32 v229, v212 offset:1536
	ds_read_b32 v230, v212 offset:2048
	ds_read_b32 v231, v212 offset:2560
	ds_read_b32 v232, v212 offset:3072
	ds_read_b32 v233, v212 offset:3584
	ds_read_b32 v234, v212 offset:4096
	ds_read_b32 v235, v212 offset:4608
	ds_read_b32 v236, v212 offset:5120
	ds_read_b32 v237, v212 offset:5632
	ds_read_b32 v238, v212 offset:6144
	ds_read_b32 v239, v212 offset:6656
	ds_read_b32 v240, v212 offset:7168
	ds_read_b32 v241, v212 offset:7680
	s_waitcnt lgkmcnt(0)
	v_max_f32_e32 v226, v226, v226
	v_max_f32_e32 v227, v227, v227
	v_max_f32_e32 v228, v228, v228
	v_max_f32_e32 v229, v229, v229
	v_max_f32_e32 v230, v230, v230
	v_max_f32_e32 v231, v231, v231
	v_max_f32_e32 v232, v232, v232
	v_max_f32_e32 v233, v233, v233
	v_max_f32_e32 v234, v234, v234
	v_max_f32_e32 v235, v235, v235
	v_max_f32_e32 v236, v236, v236
	v_max_f32_e32 v237, v237, v237
	v_max_f32_e32 v238, v238, v238
	v_max_f32_e32 v239, v239, v239
	v_max_f32_e32 v240, v240, v240
	v_max_f32_e32 v241, v241, v241
	v_med3_f32 v226, v226, s62, v95
	v_med3_f32 v227, v227, s62, v95
	v_med3_f32 v228, v228, s62, v95
	v_med3_f32 v229, v229, s62, v95
	v_med3_f32 v230, v230, s62, v95
	v_med3_f32 v231, v231, s62, v95
	v_med3_f32 v232, v232, s62, v95
	v_med3_f32 v233, v233, s62, v95
	v_med3_f32 v234, v234, s62, v95
	v_med3_f32 v235, v235, s62, v95
	v_med3_f32 v236, v236, s62, v95
	v_med3_f32 v237, v237, s62, v95
	v_med3_f32 v238, v238, s62, v95
	v_med3_f32 v239, v239, s62, v95
	v_med3_f32 v240, v240, s62, v95
	v_med3_f32 v241, v241, s62, v95
	v_mov_b32_e32 v242, 0
	v_mov_b32_e32 v243, 0
	v_mov_b32_e32 v244, 0
	v_mov_b32_e32 v245, 0
	v_cvt_pk_fp8_f32 v242, v226, v227
	v_cvt_pk_fp8_f32 v243, v230, v231
	v_cvt_pk_fp8_f32 v244, v234, v235
	v_cvt_pk_fp8_f32 v245, v238, v239
	v_cvt_pk_fp8_f32 v242, v228, v229 op_sel:[0,0,1]
	v_cvt_pk_fp8_f32 v243, v232, v233 op_sel:[0,0,1]
	v_cvt_pk_fp8_f32 v244, v236, v237 op_sel:[0,0,1]
	v_cvt_pk_fp8_f32 v245, v240, v241 op_sel:[0,0,1]
	s_nop 0
	global_store_dwordx4 v77, v[242:245], s[6:7]
	ds_read_b32 v226, v214
	ds_read_b32 v227, v214 offset:512
	ds_read_b32 v228, v214 offset:1024
	ds_read_b32 v229, v214 offset:1536
	ds_read_b32 v230, v214 offset:2048
	ds_read_b32 v231, v214 offset:2560
	ds_read_b32 v232, v214 offset:3072
	ds_read_b32 v233, v214 offset:3584
	ds_read_b32 v234, v214 offset:4096
	ds_read_b32 v235, v214 offset:4608
	ds_read_b32 v236, v214 offset:5120
	ds_read_b32 v237, v214 offset:5632
	ds_read_b32 v238, v214 offset:6144
	ds_read_b32 v239, v214 offset:6656
	ds_read_b32 v240, v214 offset:7168
	ds_read_b32 v241, v214 offset:7680
	s_waitcnt lgkmcnt(0)
	v_max_f32_e32 v226, v226, v226
	v_max_f32_e32 v227, v227, v227
	v_max_f32_e32 v228, v228, v228
	v_max_f32_e32 v229, v229, v229
	v_max_f32_e32 v230, v230, v230
	v_max_f32_e32 v231, v231, v231
	v_max_f32_e32 v232, v232, v232
	v_max_f32_e32 v233, v233, v233
	v_max_f32_e32 v234, v234, v234
	v_max_f32_e32 v235, v235, v235
	v_max_f32_e32 v236, v236, v236
	v_max_f32_e32 v237, v237, v237
	v_max_f32_e32 v238, v238, v238
	v_max_f32_e32 v239, v239, v239
	v_max_f32_e32 v240, v240, v240
	v_max_f32_e32 v241, v241, v241
	v_med3_f32 v226, v226, s62, v95
	v_med3_f32 v227, v227, s62, v95
	v_med3_f32 v228, v228, s62, v95
	v_med3_f32 v229, v229, s62, v95
	v_med3_f32 v230, v230, s62, v95
	v_med3_f32 v231, v231, s62, v95
	v_med3_f32 v232, v232, s62, v95
	v_med3_f32 v233, v233, s62, v95
	v_med3_f32 v234, v234, s62, v95
	v_med3_f32 v235, v235, s62, v95
	v_med3_f32 v236, v236, s62, v95
	v_med3_f32 v237, v237, s62, v95
	v_med3_f32 v238, v238, s62, v95
	v_med3_f32 v239, v239, s62, v95
	v_med3_f32 v240, v240, s62, v95
	v_med3_f32 v241, v241, s62, v95
	v_mov_b32_e32 v242, 0
	v_mov_b32_e32 v243, 0
	v_mov_b32_e32 v244, 0
	v_mov_b32_e32 v245, 0
	v_cvt_pk_fp8_f32 v242, v226, v227
	v_cvt_pk_fp8_f32 v243, v230, v231
	v_cvt_pk_fp8_f32 v244, v234, v235
	v_cvt_pk_fp8_f32 v245, v238, v239
	v_cvt_pk_fp8_f32 v242, v228, v229 op_sel:[0,0,1]
	v_cvt_pk_fp8_f32 v243, v232, v233 op_sel:[0,0,1]
	v_cvt_pk_fp8_f32 v244, v236, v237 op_sel:[0,0,1]
	v_cvt_pk_fp8_f32 v245, v240, v241 op_sel:[0,0,1]
	s_nop 0
	global_store_dwordx4 v78, v[242:245], s[6:7]
	s_waitcnt vmcnt(12)
	v_mul_f32_e32 v144, v34, v144
	v_mul_f32_e32 v145, v34, v145
	v_mul_f32_e32 v146, v34, v146
	v_mul_f32_e32 v147, v34, v147
	ds_write_b128 v209, v[144:147]
	v_mul_f32_e32 v148, v35, v148
	v_mul_f32_e32 v149, v35, v149
	v_mul_f32_e32 v150, v35, v150
	v_mul_f32_e32 v151, v35, v151
	ds_write_b128 v209, v[148:151] offset:1024
	v_mul_f32_e32 v152, v36, v152
	v_mul_f32_e32 v153, v36, v153
	v_mul_f32_e32 v154, v36, v154
	v_mul_f32_e32 v155, v36, v155
	ds_write_b128 v209, v[152:155] offset:2048
	v_mul_f32_e32 v156, v37, v156
	v_mul_f32_e32 v157, v37, v157
	v_mul_f32_e32 v158, v37, v158
	v_mul_f32_e32 v159, v37, v159
	ds_write_b128 v209, v[156:159] offset:3072
	v_mul_f32_e32 v160, v38, v160
	v_mul_f32_e32 v161, v38, v161
	v_mul_f32_e32 v162, v38, v162
	v_mul_f32_e32 v163, v38, v163
	ds_write_b128 v209, v[160:163] offset:4096
	v_mul_f32_e32 v164, v39, v164
	v_mul_f32_e32 v165, v39, v165
	v_mul_f32_e32 v166, v39, v166
	v_mul_f32_e32 v167, v39, v167
	ds_write_b128 v209, v[164:167] offset:5120
	v_mul_f32_e32 v168, v40, v168
	v_mul_f32_e32 v169, v40, v169
	v_mul_f32_e32 v170, v40, v170
	v_mul_f32_e32 v171, v40, v171
	ds_write_b128 v209, v[168:171] offset:6144
	v_mul_f32_e32 v172, v41, v172
	v_mul_f32_e32 v173, v41, v173
	v_mul_f32_e32 v174, v41, v174
	v_mul_f32_e32 v175, v41, v175
	ds_write_b128 v209, v[172:175] offset:7168
	s_waitcnt lgkmcnt(0)
	s_barrier
; #define GAS __attribute__((address_space(1)))
; #define LAS __attribute__((address_space(3)))
; #define LDS_WAIT() asm volatile("s_waitcnt lgkmcnt(0)" ::: "memory")
; __device__ __forceinline__ unsigned pk4_fp8(float a, float b, float c, float d) {
;     a = fminf(fmaxf(a, -448.f), 448.f); b = fminf(fmaxf(b, -448.f), 448.f); c = fminf(fmaxf(c, -448.f), 448.f); d = fminf(fmaxf(d, -448.f), 448.f);
;     int w = __builtin_amdgcn_cvt_pk_fp8_f32(a, b, 0, false); w = __builtin_amdgcn_cvt_pk_fp8_f32(c, d, w, true); return (unsigned)w; }
;     const int pr = item >> 1, kb = 2 * (pr / nblk) + (item & 1), nb = pr % nblk, k0 = 64 * kb, n0 = 32 * nb;
;     const int nr = n0 + (lane & 31); const int sc = MAP == 1 ? src_col_in(nr) : nr;
;     float v[32];
; #pragma unroll
;     for (int i = 0; i < 32; ++i) v[i] = sc >= 0 ? W[(size_t)(k0 + 2 * i + (lane >> 5)) * Nsrc + sc] : 0.f;
; #pragma unroll
;     for (int i = 0; i < 32; ++i) { const int k = k0 + 2 * i + (lane >> 5); float x = v[i] * wscale; if (KS) x *= (k < ksplit ? ksA[k] : ksB[k - ksplit]); scr[(2 * i + (lane >> 5)) * 33 + (lane & 31)] = x; }
;     LDS_WAIT(); asm volatile("" ::: "memory");
;     const int c = lane & 7;
; #pragma unroll
;     for (int j = 0; j < 4; ++j) { const int n = (lane >> 3) + 8 * j; const LAS float* s = scr + (8 * c) * 33 + n;
;         const unsigned long long o = (unsigned long long)pg8::pk4_fp8(s[0 * 33], s[1 * 33], s[2 * 33], s[3 * 33]) | ((unsigned long long)pg8::pk4_fp8(s[4 * 33], s[5 * 33], s[6 * 33], s[7 * 33]) << 32);
;         *(GAS unsigned long long*)(WT + (size_t)(n0 + n) * K + k0 + 8 * c) = o; }
;     LDS_WAIT(); asm volatile("" ::: "memory");
	s_add_u32 s8, s34, 0x6000
	s_addc_u32 s9, s35, 0
	global_load_dwordx4 v[144:147], v74, s[8:9]
	s_add_u32 s8, s8, 0x20000
	s_addc_u32 s9, s9, 0
	global_load_dwordx4 v[148:151], v74, s[8:9]
	s_add_u32 s8, s8, 0x20000
	s_addc_u32 s9, s9, 0
	global_load_dwordx4 v[152:155], v74, s[8:9]
	s_add_u32 s8, s8, 0x20000
	s_addc_u32 s9, s9, 0
	global_load_dwordx4 v[156:159], v74, s[8:9]
	s_add_u32 s8, s8, 0x20000
	s_addc_u32 s9, s9, 0
	global_load_dwordx4 v[160:163], v74, s[8:9]
	s_add_u32 s8, s8, 0x20000
	s_addc_u32 s9, s9, 0
	global_load_dwordx4 v[164:167], v74, s[8:9]
	s_add_u32 s8, s8, 0x20000
	s_addc_u32 s9, s9, 0
	global_load_dwordx4 v[168:171], v74, s[8:9]
	s_add_u32 s8, s8, 0x20000
	s_addc_u32 s9, s9, 0
	global_load_dwordx4 v[172:175], v74, s[8:9]
	s_add_u32 s6, s36, 0x1000000
	s_addc_u32 s7, s37, 0
	ds_read_b32 v226, v211
	ds_read_b32 v227, v211 offset:512
	ds_read_b32 v228, v211 offset:1024
	ds_read_b32 v229, v211 offset:1536
	ds_read_b32 v230, v211 offset:2048
	ds_read_b32 v231, v211 offset:2560
	ds_read_b32 v232, v211 offset:3072
	ds_read_b32 v233, v211 offset:3584
	ds_read_b32 v234, v211 offset:4096
	ds_read_b32 v235, v211 offset:4608
	ds_read_b32 v236, v211 offset:5120
	ds_read_b32 v237, v211 offset:5632
	ds_read_b32 v238, v211 offset:6144
	ds_read_b32 v239, v211 offset:6656
	ds_read_b32 v240, v211 offset:7168
	ds_read_b32 v241, v211 offset:7680
	s_waitcnt lgkmcnt(0)
	v_max_f32_e32 v226, v226, v226
	v_max_f32_e32 v227, v227, v227
	v_max_f32_e32 v228, v228, v228
	v_max_f32_e32 v229, v229, v229
	v_max_f32_e32 v230, v230, v230
	v_max_f32_e32 v231, v231, v231
	v_max_f32_e32 v232, v232, v232
	v_max_f32_e32 v233, v233, v233
	v_max_f32_e32 v234, v234, v234
	v_max_f32_e32 v235, v235, v235
	v_max_f32_e32 v236, v236, v236
	v_max_f32_e32 v237, v237, v237
	v_max_f32_e32 v238, v238, v238
	v_max_f32_e32 v239, v239, v239
	v_max_f32_e32 v240, v240, v240
	v_max_f32_e32 v241, v241, v241
	v_med3_f32 v226, v226, s62, v95
	v_med3_f32 v227, v227, s62, v95
	v_med3_f32 v228, v228, s62, v95
	v_med3_f32 v229, v229, s62, v95
	v_med3_f32 v230, v230, s62, v95
	v_med3_f32 v231, v231, s62, v95
	v_med3_f32 v232, v232, s62, v95
	v_med3_f32 v233, v233, s62, v95
	v_med3_f32 v234, v234, s62, v95
	v_med3_f32 v235, v235, s62, v95
	v_med3_f32 v236, v236, s62, v95
	v_med3_f32 v237, v237, s62, v95
	v_med3_f32 v238, v238, s62, v95
	v_med3_f32 v239, v239, s62, v95
	v_med3_f32 v240, v240, s62, v95
	v_med3_f32 v241, v241, s62, v95
	v_mov_b32_e32 v242, 0
	v_mov_b32_e32 v243, 0
	v_mov_b32_e32 v244, 0
	v_mov_b32_e32 v245, 0
	v_cvt_pk_fp8_f32 v242, v226, v227
	v_cvt_pk_fp8_f32 v243, v230, v231
	v_cvt_pk_fp8_f32 v244, v234, v235
	v_cvt_pk_fp8_f32 v245, v238, v239
	v_cvt_pk_fp8_f32 v242, v228, v229 op_sel:[0,0,1]
	v_cvt_pk_fp8_f32 v243, v232, v233 op_sel:[0,0,1]
	v_cvt_pk_fp8_f32 v244, v236, v237 op_sel:[0,0,1]
	v_cvt_pk_fp8_f32 v245, v240, v241 op_sel:[0,0,1]
	s_nop 0
	global_store_dwordx4 v77, v[242:245], s[6:7]
	ds_read_b32 v226, v213
	ds_read_b32 v227, v213 offset:512
	ds_read_b32 v228, v213 offset:1024
	ds_read_b32 v229, v213 offset:1536
	ds_read_b32 v230, v213 offset:2048
	ds_read_b32 v231, v213 offset:2560
	ds_read_b32 v232, v213 offset:3072
	ds_read_b32 v233, v213 offset:3584
	ds_read_b32 v234, v213 offset:4096
	ds_read_b32 v235, v213 offset:4608
	ds_read_b32 v236, v213 offset:5120
	ds_read_b32 v237, v213 offset:5632
	ds_read_b32 v238, v213 offset:6144
	ds_read_b32 v239, v213 offset:6656
	ds_read_b32 v240, v213 offset:7168
	ds_read_b32 v241, v213 offset:7680
	s_waitcnt lgkmcnt(0)
	v_max_f32_e32 v226, v226, v226
	v_max_f32_e32 v227, v227, v227
	v_max_f32_e32 v228, v228, v228
	v_max_f32_e32 v229, v229, v229
	v_max_f32_e32 v230, v230, v230
	v_max_f32_e32 v231, v231, v231
	v_max_f32_e32 v232, v232, v232
	v_max_f32_e32 v233, v233, v233
	v_max_f32_e32 v234, v234, v234
	v_max_f32_e32 v235, v235, v235
	v_max_f32_e32 v236, v236, v236
	v_max_f32_e32 v237, v237, v237
	v_max_f32_e32 v238, v238, v238
	v_max_f32_e32 v239, v239, v239
	v_max_f32_e32 v240, v240, v240
	v_max_f32_e32 v241, v241, v241
	v_med3_f32 v226, v226, s62, v95
	v_med3_f32 v227, v227, s62, v95
	v_med3_f32 v228, v228, s62, v95
	v_med3_f32 v229, v229, s62, v95
	v_med3_f32 v230, v230, s62, v95
	v_med3_f32 v231, v231, s62, v95
	v_med3_f32 v232, v232, s62, v95
	v_med3_f32 v233, v233, s62, v95
	v_med3_f32 v234, v234, s62, v95
	v_med3_f32 v235, v235, s62, v95
	v_med3_f32 v236, v236, s62, v95
	v_med3_f32 v237, v237, s62, v95
	v_med3_f32 v238, v238, s62, v95
	v_med3_f32 v239, v239, s62, v95
	v_med3_f32 v240, v240, s62, v95
	v_med3_f32 v241, v241, s62, v95
	v_mov_b32_e32 v242, 0
	v_mov_b32_e32 v243, 0
	v_mov_b32_e32 v244, 0
	v_mov_b32_e32 v245, 0
	v_cvt_pk_fp8_f32 v242, v226, v227
	v_cvt_pk_fp8_f32 v243, v230, v231
	v_cvt_pk_fp8_f32 v244, v234, v235
	v_cvt_pk_fp8_f32 v245, v238, v239
	v_cvt_pk_fp8_f32 v242, v228, v229 op_sel:[0,0,1]
	v_cvt_pk_fp8_f32 v243, v232, v233 op_sel:[0,0,1]
	v_cvt_pk_fp8_f32 v244, v236, v237 op_sel:[0,0,1]
	v_cvt_pk_fp8_f32 v245, v240, v241 op_sel:[0,0,1]
	s_nop 0
	global_store_dwordx4 v78, v[242:245], s[6:7]
	s_waitcnt vmcnt(12)
	v_mul_f32_e32 v176, v34, v176
	v_mul_f32_e32 v177, v34, v177
	v_mul_f32_e32 v178, v34, v178
	v_mul_f32_e32 v179, v34, v179
	ds_write_b128 v210, v[176:179]
	v_mul_f32_e32 v180, v35, v180
	v_mul_f32_e32 v181, v35, v181
	v_mul_f32_e32 v182, v35, v182
	v_mul_f32_e32 v183, v35, v183
	ds_write_b128 v210, v[180:183] offset:1024
	v_mul_f32_e32 v184, v36, v184
	v_mul_f32_e32 v185, v36, v185
	v_mul_f32_e32 v186, v36, v186
	v_mul_f32_e32 v187, v36, v187
	ds_write_b128 v210, v[184:187] offset:2048
	v_mul_f32_e32 v188, v37, v188
	v_mul_f32_e32 v189, v37, v189
	v_mul_f32_e32 v190, v37, v190
	v_mul_f32_e32 v191, v37, v191
	ds_write_b128 v210, v[188:191] offset:3072
	v_mul_f32_e32 v192, v38, v192
	v_mul_f32_e32 v193, v38, v193
	v_mul_f32_e32 v194, v38, v194
	v_mul_f32_e32 v195, v38, v195
	ds_write_b128 v210, v[192:195] offset:4096
	v_mul_f32_e32 v196, v39, v196
	v_mul_f32_e32 v197, v39, v197
	v_mul_f32_e32 v198, v39, v198
	v_mul_f32_e32 v199, v39, v199
	ds_write_b128 v210, v[196:199] offset:5120
	v_mul_f32_e32 v200, v40, v200
	v_mul_f32_e32 v201, v40, v201
	v_mul_f32_e32 v202, v40, v202
	v_mul_f32_e32 v203, v40, v203
	ds_write_b128 v210, v[200:203] offset:6144
	v_mul_f32_e32 v204, v41, v204
	v_mul_f32_e32 v205, v41, v205
	v_mul_f32_e32 v206, v41, v206
	v_mul_f32_e32 v207, v41, v207
	ds_write_b128 v210, v[204:207] offset:7168
	s_waitcnt lgkmcnt(0)
	s_barrier
; #define GAS __attribute__((address_space(1)))
; #define LAS __attribute__((address_space(3)))
; #define LDS_WAIT() asm volatile("s_waitcnt lgkmcnt(0)" ::: "memory")
; __device__ __forceinline__ unsigned pk4_fp8(float a, float b, float c, float d) {
;     a = fminf(fmaxf(a, -448.f), 448.f); b = fminf(fmaxf(b, -448.f), 448.f); c = fminf(fmaxf(c, -448.f), 448.f); d = fminf(fmaxf(d, -448.f), 448.f);
;     int w = __builtin_amdgcn_cvt_pk_fp8_f32(a, b, 0, false); w = __builtin_amdgcn_cvt_pk_fp8_f32(c, d, w, true); return (unsigned)w; }
;     const int pr = item >> 1, kb = 2 * (pr / nblk) + (item & 1), nb = pr % nblk, k0 = 64 * kb, n0 = 32 * nb;
;     const int nr = n0 + (lane & 31); const int sc = MAP == 1 ? src_col_in(nr) : nr;
;     float v[32];
; #pragma unroll
;     for (int i = 0; i < 32; ++i) v[i] = sc >= 0 ? W[(size_t)(k0 + 2 * i + (lane >> 5)) * Nsrc + sc] : 0.f;
; #pragma unroll
;     for (int i = 0; i < 32; ++i) { const int k = k0 + 2 * i + (lane >> 5); float x = v[i] * wscale; if (KS) x *= (k < ksplit ? ksA[k] : ksB[k - ksplit]); scr[(2 * i + (lane >> 5)) * 33 + (lane & 31)] = x; }
;     LDS_WAIT(); asm volatile("" ::: "memory");
;     const int c = lane & 7;
; #pragma unroll
;     for (int j = 0; j < 4; ++j) { const int n = (lane >> 3) + 8 * j; const LAS float* s = scr + (8 * c) * 33 + n;
;         const unsigned long long o = (unsigned long long)pg8::pk4_fp8(s[0 * 33], s[1 * 33], s[2 * 33], s[3 * 33]) | ((unsigned long long)pg8::pk4_fp8(s[4 * 33], s[5 * 33], s[6 * 33], s[7 * 33]) << 32);
;         *(GAS unsigned long long*)(WT + (size_t)(n0 + n) * K + k0 + 8 * c) = o; }
;     LDS_WAIT(); asm volatile("" ::: "memory");
	s_add_u32 s8, s34, 0x7000
	s_addc_u32 s9, s35, 0
	global_load_dwordx4 v[176:179], v74, s[8:9]
	s_add_u32 s8, s8, 0x20000
	s_addc_u32 s9, s9, 0
	global_load_dwordx4 v[180:183], v74, s[8:9]
	s_add_u32 s8, s8, 0x20000
	s_addc_u32 s9, s9, 0
	global_load_dwordx4 v[184:187], v74, s[8:9]
	s_add_u32 s8, s8, 0x20000
	s_addc_u32 s9, s9, 0
	global_load_dwordx4 v[188:191], v74, s[8:9]
	s_add_u32 s8, s8, 0x20000
	s_addc_u32 s9, s9, 0
	global_load_dwordx4 v[192:195], v74, s[8:9]
	s_add_u32 s8, s8, 0x20000
	s_addc_u32 s9, s9, 0
	global_load_dwordx4 v[196:199], v74, s[8:9]
	s_add_u32 s8, s8, 0x20000
	s_addc_u32 s9, s9, 0
	global_load_dwordx4 v[200:203], v74, s[8:9]
	s_add_u32 s8, s8, 0x20000
	s_addc_u32 s9, s9, 0
	global_load_dwordx4 v[204:207], v74, s[8:9]
	s_add_u32 s6, s36, 0x1400000
	s_addc_u32 s7, s37, 0
	ds_read_b32 v226, v212
	ds_read_b32 v227, v212 offset:512
	ds_read_b32 v228, v212 offset:1024
	ds_read_b32 v229, v212 offset:1536
	ds_read_b32 v230, v212 offset:2048
	ds_read_b32 v231, v212 offset:2560
	ds_read_b32 v232, v212 offset:3072
	ds_read_b32 v233, v212 offset:3584
	ds_read_b32 v234, v212 offset:4096
	ds_read_b32 v235, v212 offset:4608
	ds_read_b32 v236, v212 offset:5120
	ds_read_b32 v237, v212 offset:5632
	ds_read_b32 v238, v212 offset:6144
	ds_read_b32 v239, v212 offset:6656
	ds_read_b32 v240, v212 offset:7168
	ds_read_b32 v241, v212 offset:7680
	s_waitcnt lgkmcnt(0)
	v_max_f32_e32 v226, v226, v226
	v_max_f32_e32 v227, v227, v227
	v_max_f32_e32 v228, v228, v228
	v_max_f32_e32 v229, v229, v229
	v_max_f32_e32 v230, v230, v230
	v_max_f32_e32 v231, v231, v231
	v_max_f32_e32 v232, v232, v232
	v_max_f32_e32 v233, v233, v233
	v_max_f32_e32 v234, v234, v234
	v_max_f32_e32 v235, v235, v235
	v_max_f32_e32 v236, v236, v236
	v_max_f32_e32 v237, v237, v237
	v_max_f32_e32 v238, v238, v238
	v_max_f32_e32 v239, v239, v239
	v_max_f32_e32 v240, v240, v240
	v_max_f32_e32 v241, v241, v241
	v_med3_f32 v226, v226, s62, v95
	v_med3_f32 v227, v227, s62, v95
	v_med3_f32 v228, v228, s62, v95
	v_med3_f32 v229, v229, s62, v95
	v_med3_f32 v230, v230, s62, v95
	v_med3_f32 v231, v231, s62, v95
	v_med3_f32 v232, v232, s62, v95
	v_med3_f32 v233, v233, s62, v95
	v_med3_f32 v234, v234, s62, v95
	v_med3_f32 v235, v235, s62, v95
	v_med3_f32 v236, v236, s62, v95
	v_med3_f32 v237, v237, s62, v95
	v_med3_f32 v238, v238, s62, v95
	v_med3_f32 v239, v239, s62, v95
	v_med3_f32 v240, v240, s62, v95
	v_med3_f32 v241, v241, s62, v95
	v_mov_b32_e32 v242, 0
	v_mov_b32_e32 v243, 0
	v_mov_b32_e32 v244, 0
	v_mov_b32_e32 v245, 0
	v_cvt_pk_fp8_f32 v242, v226, v227
	v_cvt_pk_fp8_f32 v243, v230, v231
	v_cvt_pk_fp8_f32 v244, v234, v235
	v_cvt_pk_fp8_f32 v245, v238, v239
	v_cvt_pk_fp8_f32 v242, v228, v229 op_sel:[0,0,1]
	v_cvt_pk_fp8_f32 v243, v232, v233 op_sel:[0,0,1]
	v_cvt_pk_fp8_f32 v244, v236, v237 op_sel:[0,0,1]
	v_cvt_pk_fp8_f32 v245, v240, v241 op_sel:[0,0,1]
	s_nop 0
	global_store_dwordx4 v77, v[242:245], s[6:7]
	ds_read_b32 v226, v214
	ds_read_b32 v227, v214 offset:512
	ds_read_b32 v228, v214 offset:1024
	ds_read_b32 v229, v214 offset:1536
	ds_read_b32 v230, v214 offset:2048
	ds_read_b32 v231, v214 offset:2560
	ds_read_b32 v232, v214 offset:3072
	ds_read_b32 v233, v214 offset:3584
	ds_read_b32 v234, v214 offset:4096
	ds_read_b32 v235, v214 offset:4608
	ds_read_b32 v236, v214 offset:5120
	ds_read_b32 v237, v214 offset:5632
	ds_read_b32 v238, v214 offset:6144
	ds_read_b32 v239, v214 offset:6656
	ds_read_b32 v240, v214 offset:7168
	ds_read_b32 v241, v214 offset:7680
	s_waitcnt lgkmcnt(0)
	v_max_f32_e32 v226, v226, v226
	v_max_f32_e32 v227, v227, v227
	v_max_f32_e32 v228, v228, v228
	v_max_f32_e32 v229, v229, v229
	v_max_f32_e32 v230, v230, v230
	v_max_f32_e32 v231, v231, v231
	v_max_f32_e32 v232, v232, v232
	v_max_f32_e32 v233, v233, v233
	v_max_f32_e32 v234, v234, v234
	v_max_f32_e32 v235, v235, v235
	v_max_f32_e32 v236, v236, v236
	v_max_f32_e32 v237, v237, v237
	v_max_f32_e32 v238, v238, v238
	v_max_f32_e32 v239, v239, v239
	v_max_f32_e32 v240, v240, v240
	v_max_f32_e32 v241, v241, v241
	v_med3_f32 v226, v226, s62, v95
	v_med3_f32 v227, v227, s62, v95
	v_med3_f32 v228, v228, s62, v95
	v_med3_f32 v229, v229, s62, v95
	v_med3_f32 v230, v230, s62, v95
	v_med3_f32 v231, v231, s62, v95
	v_med3_f32 v232, v232, s62, v95
	v_med3_f32 v233, v233, s62, v95
	v_med3_f32 v234, v234, s62, v95
	v_med3_f32 v235, v235, s62, v95
	v_med3_f32 v236, v236, s62, v95
	v_med3_f32 v237, v237, s62, v95
	v_med3_f32 v238, v238, s62, v95
	v_med3_f32 v239, v239, s62, v95
	v_med3_f32 v240, v240, s62, v95
	v_med3_f32 v241, v241, s62, v95
	v_mov_b32_e32 v242, 0
	v_mov_b32_e32 v243, 0
	v_mov_b32_e32 v244, 0
	v_mov_b32_e32 v245, 0
	v_cvt_pk_fp8_f32 v242, v226, v227
	v_cvt_pk_fp8_f32 v243, v230, v231
	v_cvt_pk_fp8_f32 v244, v234, v235
	v_cvt_pk_fp8_f32 v245, v238, v239
	v_cvt_pk_fp8_f32 v242, v228, v229 op_sel:[0,0,1]
	v_cvt_pk_fp8_f32 v243, v232, v233 op_sel:[0,0,1]
	v_cvt_pk_fp8_f32 v244, v236, v237 op_sel:[0,0,1]
	v_cvt_pk_fp8_f32 v245, v240, v241 op_sel:[0,0,1]
	s_nop 0
	global_store_dwordx4 v78, v[242:245], s[6:7]
	s_waitcnt vmcnt(12)
	v_mul_f32_e32 v144, v34, v144
	v_mul_f32_e32 v145, v34, v145
	v_mul_f32_e32 v146, v34, v146
	v_mul_f32_e32 v147, v34, v147
	ds_write_b128 v209, v[144:147]
	v_mul_f32_e32 v148, v35, v148
	v_mul_f32_e32 v149, v35, v149
	v_mul_f32_e32 v150, v35, v150
	v_mul_f32_e32 v151, v35, v151
	ds_write_b128 v209, v[148:151] offset:1024
	v_mul_f32_e32 v152, v36, v152
	v_mul_f32_e32 v153, v36, v153
	v_mul_f32_e32 v154, v36, v154
	v_mul_f32_e32 v155, v36, v155
	ds_write_b128 v209, v[152:155] offset:2048
	v_mul_f32_e32 v156, v37, v156
	v_mul_f32_e32 v157, v37, v157
	v_mul_f32_e32 v158, v37, v158
	v_mul_f32_e32 v159, v37, v159
	ds_write_b128 v209, v[156:159] offset:3072
	v_mul_f32_e32 v160, v38, v160
	v_mul_f32_e32 v161, v38, v161
	v_mul_f32_e32 v162, v38, v162
	v_mul_f32_e32 v163, v38, v163
	ds_write_b128 v209, v[160:163] offset:4096
	v_mul_f32_e32 v164, v39, v164
	v_mul_f32_e32 v165, v39, v165
	v_mul_f32_e32 v166, v39, v166
	v_mul_f32_e32 v167, v39, v167
	ds_write_b128 v209, v[164:167] offset:5120
	v_mul_f32_e32 v168, v40, v168
	v_mul_f32_e32 v169, v40, v169
	v_mul_f32_e32 v170, v40, v170
	v_mul_f32_e32 v171, v40, v171
	ds_write_b128 v209, v[168:171] offset:6144
	v_mul_f32_e32 v172, v41, v172
	v_mul_f32_e32 v173, v41, v173
	v_mul_f32_e32 v174, v41, v174
	v_mul_f32_e32 v175, v41, v175
	ds_write_b128 v209, v[172:175] offset:7168
	s_waitcnt lgkmcnt(0)
	s_barrier
; #define GAS __attribute__((address_space(1)))
; #define LAS __attribute__((address_space(3)))
; #define LDS_WAIT() asm volatile("s_waitcnt lgkmcnt(0)" ::: "memory")
; __device__ __forceinline__ unsigned pk4_fp8(float a, float b, float c, float d) {
;     a = fminf(fmaxf(a, -448.f), 448.f); b = fminf(fmaxf(b, -448.f), 448.f); c = fminf(fmaxf(c, -448.f), 448.f); d = fminf(fmaxf(d, -448.f), 448.f);
;     int w = __builtin_amdgcn_cvt_pk_fp8_f32(a, b, 0, false); w = __builtin_amdgcn_cvt_pk_fp8_f32(c, d, w, true); return (unsigned)w; }
;     ...
; #pragma unroll
;     for (int i = 0; i < 32; ++i) v[i] = sc >= 0 ? W[(size_t)(k0 + 2 * i + (lane >> 5)) * Nsrc + sc] : 0.f;
; #pragma unroll
;     for (int i = 0; i < 32; ++i) { const int k = k0 + 2 * i + (lane >> 5); float x = v[i] * wscale; if (KS) x *= (k < ksplit ? ksA[k] : ksB[k - ksplit]); scr[(2 * i + (lane >> 5)) * 33 + (lane & 31)] = x; }
;     LDS_WAIT(); asm volatile("" ::: "memory");
;     const int c = lane & 7;
; #pragma unroll
;     for (int j = 0; j < 4; ++j) { const int n = (lane >> 3) + 8 * j; const LAS float* s = scr + (8 * c) * 33 + n;
;         const unsigned long long o = (unsigned long long)pg8::pk4_fp8(s[0 * 33], s[1 * 33], s[2 * 33], s[3 * 33]) | ((unsigned long long)pg8::pk4_fp8(s[4 * 33], s[5 * 33], s[6 * 33], s[7 * 33]) << 32);
;         *(GAS unsigned long long*)(WT + (size_t)(n0 + n) * K + k0 + 8 * c) = o; }
;     LDS_WAIT(); asm volatile("" ::: "memory");
	s_add_u32 s8, s34, 0x8000
	s_addc_u32 s9, s35, 0
	global_load_dwordx4 v[144:147], v74, s[8:9]
	s_add_u32 s8, s8, 0x20000
	s_addc_u32 s9, s9, 0
	global_load_dwordx4 v[148:151], v74, s[8:9]
	s_add_u32 s8, s8, 0x20000
	s_addc_u32 s9, s9, 0
	global_load_dwordx4 v[152:155], v74, s[8:9]
	s_add_u32 s8, s8, 0x20000
	s_addc_u32 s9, s9, 0
	global_load_dwordx4 v[156:159], v74, s[8:9]
	s_add_u32 s8, s8, 0x20000
	s_addc_u32 s9, s9, 0
	global_load_dwordx4 v[160:163], v74, s[8:9]
	s_add_u32 s8, s8, 0x20000
	s_addc_u32 s9, s9, 0
	global_load_dwordx4 v[164:167], v74, s[8:9]
	s_add_u32 s8, s8, 0x20000
	s_addc_u32 s9, s9, 0
	global_load_dwordx4 v[168:171], v74, s[8:9]
	s_add_u32 s8, s8, 0x20000
	s_addc_u32 s9, s9, 0
	global_load_dwordx4 v[172:175], v74, s[8:9]
	s_add_u32 s6, s36, 0x1800000
	s_addc_u32 s7, s37, 0
	ds_read_b32 v226, v211
	ds_read_b32 v227, v211 offset:512
	ds_read_b32 v228, v211 offset:1024
	ds_read_b32 v229, v211 offset:1536
	ds_read_b32 v230, v211 offset:2048
	ds_read_b32 v231, v211 offset:2560
	ds_read_b32 v232, v211 offset:3072
	ds_read_b32 v233, v211 offset:3584
	ds_read_b32 v234, v211 offset:4096
	ds_read_b32 v235, v211 offset:4608
	ds_read_b32 v236, v211 offset:5120
	ds_read_b32 v237, v211 offset:5632
	ds_read_b32 v238, v211 offset:6144
	ds_read_b32 v239, v211 offset:6656
	ds_read_b32 v240, v211 offset:7168
	ds_read_b32 v241, v211 offset:7680
	s_waitcnt lgkmcnt(0)
	v_max_f32_e32 v226, v226, v226
	v_max_f32_e32 v227, v227, v227
	v_max_f32_e32 v228, v228, v228
	v_max_f32_e32 v229, v229, v229
	v_max_f32_e32 v230, v230, v230
	v_max_f32_e32 v231, v231, v231
	v_max_f32_e32 v232, v232, v232
	v_max_f32_e32 v233, v233, v233
	v_max_f32_e32 v234, v234, v234
	v_max_f32_e32 v235, v235, v235
	v_max_f32_e32 v236, v236, v236
	v_max_f32_e32 v237, v237, v237
	v_max_f32_e32 v238, v238, v238
	v_max_f32_e32 v239, v239, v239
	v_max_f32_e32 v240, v240, v240
	v_max_f32_e32 v241, v241, v241
	v_med3_f32 v226, v226, s62, v95
	v_med3_f32 v227, v227, s62, v95
	v_med3_f32 v228, v228, s62, v95
	v_med3_f32 v229, v229, s62, v95
	v_med3_f32 v230, v230, s62, v95
	v_med3_f32 v231, v231, s62, v95
	v_med3_f32 v232, v232, s62, v95
	v_med3_f32 v233, v233, s62, v95
	v_med3_f32 v234, v234, s62, v95
	v_med3_f32 v235, v235, s62, v95
	v_med3_f32 v236, v236, s62, v95
	v_med3_f32 v237, v237, s62, v95
	v_med3_f32 v238, v238, s62, v95
	v_med3_f32 v239, v239, s62, v95
	v_med3_f32 v240, v240, s62, v95
	v_med3_f32 v241, v241, s62, v95
	v_mov_b32_e32 v242, 0
	v_mov_b32_e32 v243, 0
	v_mov_b32_e32 v244, 0
	v_mov_b32_e32 v245, 0
	v_cvt_pk_fp8_f32 v242, v226, v227
	v_cvt_pk_fp8_f32 v243, v230, v231
	v_cvt_pk_fp8_f32 v244, v234, v235
	v_cvt_pk_fp8_f32 v245, v238, v239
	v_cvt_pk_fp8_f32 v242, v228, v229 op_sel:[0,0,1]
	v_cvt_pk_fp8_f32 v243, v232, v233 op_sel:[0,0,1]
	v_cvt_pk_fp8_f32 v244, v236, v237 op_sel:[0,0,1]
	v_cvt_pk_fp8_f32 v245, v240, v241 op_sel:[0,0,1]
	s_nop 0
	global_store_dwordx4 v77, v[242:245], s[6:7]
	ds_read_b32 v226, v213
	ds_read_b32 v227, v213 offset:512
	ds_read_b32 v228, v213 offset:1024
	ds_read_b32 v229, v213 offset:1536
	ds_read_b32 v230, v213 offset:2048
	ds_read_b32 v231, v213 offset:2560
	ds_read_b32 v232, v213 offset:3072
	ds_read_b32 v233, v213 offset:3584
	ds_read_b32 v234, v213 offset:4096
	ds_read_b32 v235, v213 offset:4608
	ds_read_b32 v236, v213 offset:5120
	ds_read_b32 v237, v213 offset:5632
	ds_read_b32 v238, v213 offset:6144
	ds_read_b32 v239, v213 offset:6656
	ds_read_b32 v240, v213 offset:7168
	ds_read_b32 v241, v213 offset:7680
	s_waitcnt lgkmcnt(0)
	v_max_f32_e32 v226, v226, v226
	v_max_f32_e32 v227, v227, v227
	v_max_f32_e32 v228, v228, v228
	v_max_f32_e32 v229, v229, v229
	v_max_f32_e32 v230, v230, v230
	v_max_f32_e32 v231, v231, v231
	v_max_f32_e32 v232, v232, v232
	v_max_f32_e32 v233, v233, v233
	v_max_f32_e32 v234, v234, v234
	v_max_f32_e32 v235, v235, v235
	v_max_f32_e32 v236, v236, v236
	v_max_f32_e32 v237, v237, v237
	v_max_f32_e32 v238, v238, v238
	v_max_f32_e32 v239, v239, v239
	v_max_f32_e32 v240, v240, v240
	v_max_f32_e32 v241, v241, v241
	v_med3_f32 v226, v226, s62, v95
	v_med3_f32 v227, v227, s62, v95
	v_med3_f32 v228, v228, s62, v95
	v_med3_f32 v229, v229, s62, v95
	v_med3_f32 v230, v230, s62, v95
	v_med3_f32 v231, v231, s62, v95
	v_med3_f32 v232, v232, s62, v95
	v_med3_f32 v233, v233, s62, v95
	v_med3_f32 v234, v234, s62, v95
	v_med3_f32 v235, v235, s62, v95
	v_med3_f32 v236, v236, s62, v95
	v_med3_f32 v237, v237, s62, v95
	v_med3_f32 v238, v238, s62, v95
	v_med3_f32 v239, v239, s62, v95
	v_med3_f32 v240, v240, s62, v95
	v_med3_f32 v241, v241, s62, v95
	v_mov_b32_e32 v242, 0
	v_mov_b32_e32 v243, 0
	v_mov_b32_e32 v244, 0
	v_mov_b32_e32 v245, 0
	v_cvt_pk_fp8_f32 v242, v226, v227
	v_cvt_pk_fp8_f32 v243, v230, v231
	v_cvt_pk_fp8_f32 v244, v234, v235
	v_cvt_pk_fp8_f32 v245, v238, v239
	v_cvt_pk_fp8_f32 v242, v228, v229 op_sel:[0,0,1]
	v_cvt_pk_fp8_f32 v243, v232, v233 op_sel:[0,0,1]
	v_cvt_pk_fp8_f32 v244, v236, v237 op_sel:[0,0,1]
	v_cvt_pk_fp8_f32 v245, v240, v241 op_sel:[0,0,1]
	s_nop 0
	global_store_dwordx4 v78, v[242:245], s[6:7]
	s_waitcnt vmcnt(12)
	v_mul_f32_e32 v176, v34, v176
	v_mul_f32_e32 v177, v34, v177
	v_mul_f32_e32 v178, v34, v178
	v_mul_f32_e32 v179, v34, v179
	ds_write_b128 v210, v[176:179]
	v_mul_f32_e32 v180, v35, v180
	v_mul_f32_e32 v181, v35, v181
	v_mul_f32_e32 v182, v35, v182
	v_mul_f32_e32 v183, v35, v183
	ds_write_b128 v210, v[180:183] offset:1024
	v_mul_f32_e32 v184, v36, v184
	v_mul_f32_e32 v185, v36, v185
	v_mul_f32_e32 v186, v36, v186
	v_mul_f32_e32 v187, v36, v187
	ds_write_b128 v210, v[184:187] offset:2048
	v_mul_f32_e32 v188, v37, v188
	v_mul_f32_e32 v189, v37, v189
	v_mul_f32_e32 v190, v37, v190
	v_mul_f32_e32 v191, v37, v191
	ds_write_b128 v210, v[188:191] offset:3072
	v_mul_f32_e32 v192, v38, v192
	v_mul_f32_e32 v193, v38, v193
	v_mul_f32_e32 v194, v38, v194
	v_mul_f32_e32 v195, v38, v195
	ds_write_b128 v210, v[192:195] offset:4096
	v_mul_f32_e32 v196, v39, v196
	v_mul_f32_e32 v197, v39, v197
	v_mul_f32_e32 v198, v39, v198
	v_mul_f32_e32 v199, v39, v199
	ds_write_b128 v210, v[196:199] offset:5120
	v_mul_f32_e32 v200, v40, v200
	v_mul_f32_e32 v201, v40, v201
	v_mul_f32_e32 v202, v40, v202
	v_mul_f32_e32 v203, v40, v203
	ds_write_b128 v210, v[200:203] offset:6144
	v_mul_f32_e32 v204, v41, v204
	v_mul_f32_e32 v205, v41, v205
	v_mul_f32_e32 v206, v41, v206
	v_mul_f32_e32 v207, v41, v207
	ds_write_b128 v210, v[204:207] offset:7168
	s_waitcnt lgkmcnt(0)
	s_barrier
; #define GAS __attribute__((address_space(1)))
; #define LAS __attribute__((address_space(3)))
; #define LDS_WAIT() asm volatile("s_waitcnt lgkmcnt(0)" ::: "memory")
; __device__ __forceinline__ unsigned pk4_fp8(float a, float b, float c, float d) {
;     a = fminf(fmaxf(a, -448.f), 448.f); b = fminf(fmaxf(b, -448.f), 448.f); c = fminf(fmaxf(c, -448.f), 448.f); d = fminf(fmaxf(d, -448.f), 448.f);
;     int w = __builtin_amdgcn_cvt_pk_fp8_f32(a, b, 0, false); w = __builtin_amdgcn_cvt_pk_fp8_f32(c, d, w, true); return (unsigned)w; }
;     ...
; #pragma unroll
;     for (int i = 0; i < 32; ++i) v[i] = sc >= 0 ? W[(size_t)(k0 + 2 * i + (lane >> 5)) * Nsrc + sc] : 0.f;
; #pragma unroll
;     for (int i = 0; i < 32; ++i) { const int k = k0 + 2 * i + (lane >> 5); float x = v[i] * wscale; if (KS) x *= (k < ksplit ? ksA[k] : ksB[k - ksplit]); scr[(2 * i + (lane >> 5)) * 33 + (lane & 31)] = x; }
;     LDS_WAIT(); asm volatile("" ::: "memory");
;     const int c = lane & 7;
; #pragma unroll
;     for (int j = 0; j < 4; ++j) { const int n = (lane >> 3) + 8 * j; const LAS float* s = scr + (8 * c) * 33 + n;
;         const unsigned long long o = (unsigned long long)pg8::pk4_fp8(s[0 * 33], s[1 * 33], s[2 * 33], s[3 * 33]) | ((unsigned long long)pg8::pk4_fp8(s[4 * 33], s[5 * 33], s[6 * 33], s[7 * 33]) << 32);
;         *(GAS unsigned long long*)(WT + (size_t)(n0 + n) * K + k0 + 8 * c) = o; }
;     LDS_WAIT(); asm volatile("" ::: "memory");
	s_add_u32 s8, s34, 0x9000
	s_addc_u32 s9, s35, 0
	global_load_dwordx4 v[176:179], v74, s[8:9]
	s_add_u32 s8, s8, 0x20000
	s_addc_u32 s9, s9, 0
	global_load_dwordx4 v[180:183], v74, s[8:9]
	s_add_u32 s8, s8, 0x20000
	s_addc_u32 s9, s9, 0
	global_load_dwordx4 v[184:187], v74, s[8:9]
	s_add_u32 s8, s8, 0x20000
	s_addc_u32 s9, s9, 0
	global_load_dwordx4 v[188:191], v74, s[8:9]
	s_add_u32 s8, s8, 0x20000
	s_addc_u32 s9, s9, 0
	global_load_dwordx4 v[192:195], v74, s[8:9]
	s_add_u32 s8, s8, 0x20000
	s_addc_u32 s9, s9, 0
	global_load_dwordx4 v[196:199], v74, s[8:9]
	s_add_u32 s8, s8, 0x20000
	s_addc_u32 s9, s9, 0
	global_load_dwordx4 v[200:203], v74, s[8:9]
	s_add_u32 s8, s8, 0x20000
	s_addc_u32 s9, s9, 0
	global_load_dwordx4 v[204:207], v74, s[8:9]
	s_add_u32 s6, s36, 0x1c00000
	s_addc_u32 s7, s37, 0
	ds_read_b32 v226, v212
	ds_read_b32 v227, v212 offset:512
	ds_read_b32 v228, v212 offset:1024
	ds_read_b32 v229, v212 offset:1536
	ds_read_b32 v230, v212 offset:2048
	ds_read_b32 v231, v212 offset:2560
	ds_read_b32 v232, v212 offset:3072
	ds_read_b32 v233, v212 offset:3584
	ds_read_b32 v234, v212 offset:4096
	ds_read_b32 v235, v212 offset:4608
	ds_read_b32 v236, v212 offset:5120
	ds_read_b32 v237, v212 offset:5632
	ds_read_b32 v238, v212 offset:6144
	ds_read_b32 v239, v212 offset:6656
	ds_read_b32 v240, v212 offset:7168
	ds_read_b32 v241, v212 offset:7680
	s_waitcnt lgkmcnt(0)
	v_max_f32_e32 v226, v226, v226
	v_max_f32_e32 v227, v227, v227
	v_max_f32_e32 v228, v228, v228
	v_max_f32_e32 v229, v229, v229
	v_max_f32_e32 v230, v230, v230
	v_max_f32_e32 v231, v231, v231
	v_max_f32_e32 v232, v232, v232
	v_max_f32_e32 v233, v233, v233
	v_max_f32_e32 v234, v234, v234
	v_max_f32_e32 v235, v235, v235
	v_max_f32_e32 v236, v236, v236
	v_max_f32_e32 v237, v237, v237
	v_max_f32_e32 v238, v238, v238
	v_max_f32_e32 v239, v239, v239
	v_max_f32_e32 v240, v240, v240
	v_max_f32_e32 v241, v241, v241
	v_med3_f32 v226, v226, s62, v95
	v_med3_f32 v227, v227, s62, v95
	v_med3_f32 v228, v228, s62, v95
	v_med3_f32 v229, v229, s62, v95
	v_med3_f32 v230, v230, s62, v95
	v_med3_f32 v231, v231, s62, v95
	v_med3_f32 v232, v232, s62, v95
	v_med3_f32 v233, v233, s62, v95
	v_med3_f32 v234, v234, s62, v95
	v_med3_f32 v235, v235, s62, v95
	v_med3_f32 v236, v236, s62, v95
	v_med3_f32 v237, v237, s62, v95
	v_med3_f32 v238, v238, s62, v95
	v_med3_f32 v239, v239, s62, v95
	v_med3_f32 v240, v240, s62, v95
	v_med3_f32 v241, v241, s62, v95
	v_mov_b32_e32 v242, 0
	v_mov_b32_e32 v243, 0
	v_mov_b32_e32 v244, 0
	v_mov_b32_e32 v245, 0
	v_cvt_pk_fp8_f32 v242, v226, v227
	v_cvt_pk_fp8_f32 v243, v230, v231
	v_cvt_pk_fp8_f32 v244, v234, v235
	v_cvt_pk_fp8_f32 v245, v238, v239
	v_cvt_pk_fp8_f32 v242, v228, v229 op_sel:[0,0,1]
	v_cvt_pk_fp8_f32 v243, v232, v233 op_sel:[0,0,1]
	v_cvt_pk_fp8_f32 v244, v236, v237 op_sel:[0,0,1]
	v_cvt_pk_fp8_f32 v245, v240, v241 op_sel:[0,0,1]
	s_nop 0
	global_store_dwordx4 v77, v[242:245], s[6:7]
	ds_read_b32 v226, v214
	ds_read_b32 v227, v214 offset:512
	ds_read_b32 v228, v214 offset:1024
	ds_read_b32 v229, v214 offset:1536
	ds_read_b32 v230, v214 offset:2048
	ds_read_b32 v231, v214 offset:2560
	ds_read_b32 v232, v214 offset:3072
	ds_read_b32 v233, v214 offset:3584
	ds_read_b32 v234, v214 offset:4096
	ds_read_b32 v235, v214 offset:4608
	ds_read_b32 v236, v214 offset:5120
	ds_read_b32 v237, v214 offset:5632
	ds_read_b32 v238, v214 offset:6144
	ds_read_b32 v239, v214 offset:6656
	ds_read_b32 v240, v214 offset:7168
	ds_read_b32 v241, v214 offset:7680
	s_waitcnt lgkmcnt(0)
	v_max_f32_e32 v226, v226, v226
	v_max_f32_e32 v227, v227, v227
	v_max_f32_e32 v228, v228, v228
	v_max_f32_e32 v229, v229, v229
	v_max_f32_e32 v230, v230, v230
	v_max_f32_e32 v231, v231, v231
	v_max_f32_e32 v232, v232, v232
	v_max_f32_e32 v233, v233, v233
	v_max_f32_e32 v234, v234, v234
	v_max_f32_e32 v235, v235, v235
	v_max_f32_e32 v236, v236, v236
	v_max_f32_e32 v237, v237, v237
	v_max_f32_e32 v238, v238, v238
	v_max_f32_e32 v239, v239, v239
	v_max_f32_e32 v240, v240, v240
	v_max_f32_e32 v241, v241, v241
	v_med3_f32 v226, v226, s62, v95
	v_med3_f32 v227, v227, s62, v95
	v_med3_f32 v228, v228, s62, v95
	v_med3_f32 v229, v229, s62, v95
	v_med3_f32 v230, v230, s62, v95
	v_med3_f32 v231, v231, s62, v95
	v_med3_f32 v232, v232, s62, v95
	v_med3_f32 v233, v233, s62, v95
	v_med3_f32 v234, v234, s62, v95
	v_med3_f32 v235, v235, s62, v95
	v_med3_f32 v236, v236, s62, v95
	v_med3_f32 v237, v237, s62, v95
	v_med3_f32 v238, v238, s62, v95
	v_med3_f32 v239, v239, s62, v95
	v_med3_f32 v240, v240, s62, v95
	v_med3_f32 v241, v241, s62, v95
	v_mov_b32_e32 v242, 0
	v_mov_b32_e32 v243, 0
	v_mov_b32_e32 v244, 0
	v_mov_b32_e32 v245, 0
	v_cvt_pk_fp8_f32 v242, v226, v227
	v_cvt_pk_fp8_f32 v243, v230, v231
	v_cvt_pk_fp8_f32 v244, v234, v235
	v_cvt_pk_fp8_f32 v245, v238, v239
	v_cvt_pk_fp8_f32 v242, v228, v229 op_sel:[0,0,1]
	v_cvt_pk_fp8_f32 v243, v232, v233 op_sel:[0,0,1]
	v_cvt_pk_fp8_f32 v244, v236, v237 op_sel:[0,0,1]
	v_cvt_pk_fp8_f32 v245, v240, v241 op_sel:[0,0,1]
	s_nop 0
	global_store_dwordx4 v78, v[242:245], s[6:7]
	s_waitcnt vmcnt(12)
	v_mul_f32_e32 v144, v34, v144
	v_mul_f32_e32 v145, v34, v145
	v_mul_f32_e32 v146, v34, v146
	v_mul_f32_e32 v147, v34, v147
	ds_write_b128 v209, v[144:147]
	v_mul_f32_e32 v148, v35, v148
	v_mul_f32_e32 v149, v35, v149
	v_mul_f32_e32 v150, v35, v150
	v_mul_f32_e32 v151, v35, v151
	ds_write_b128 v209, v[148:151] offset:1024
	v_mul_f32_e32 v152, v36, v152
	v_mul_f32_e32 v153, v36, v153
	v_mul_f32_e32 v154, v36, v154
	v_mul_f32_e32 v155, v36, v155
	ds_write_b128 v209, v[152:155] offset:2048
	v_mul_f32_e32 v156, v37, v156
	v_mul_f32_e32 v157, v37, v157
	v_mul_f32_e32 v158, v37, v158
	v_mul_f32_e32 v159, v37, v159
	ds_write_b128 v209, v[156:159] offset:3072
	v_mul_f32_e32 v160, v38, v160
	v_mul_f32_e32 v161, v38, v161
	v_mul_f32_e32 v162, v38, v162
	v_mul_f32_e32 v163, v38, v163
	ds_write_b128 v209, v[160:163] offset:4096
	v_mul_f32_e32 v164, v39, v164
	v_mul_f32_e32 v165, v39, v165
	v_mul_f32_e32 v166, v39, v166
	v_mul_f32_e32 v167, v39, v167
	ds_write_b128 v209, v[164:167] offset:5120
	v_mul_f32_e32 v168, v40, v168
	v_mul_f32_e32 v169, v40, v169
	v_mul_f32_e32 v170, v40, v170
	v_mul_f32_e32 v171, v40, v171
	ds_write_b128 v209, v[168:171] offset:6144
	v_mul_f32_e32 v172, v41, v172
	v_mul_f32_e32 v173, v41, v173
	v_mul_f32_e32 v174, v41, v174
	v_mul_f32_e32 v175, v41, v175
	ds_write_b128 v209, v[172:175] offset:7168
	s_waitcnt lgkmcnt(0)
	s_barrier
; #define GAS __attribute__((address_space(1)))
; #define LAS __attribute__((address_space(3)))
; #define LDS_WAIT() asm volatile("s_waitcnt lgkmcnt(0)" ::: "memory")
; __device__ __forceinline__ unsigned pk4_fp8(float a, float b, float c, float d) {
;     a = fminf(fmaxf(a, -448.f), 448.f); b = fminf(fmaxf(b, -448.f), 448.f); c = fminf(fmaxf(c, -448.f), 448.f); d = fminf(fmaxf(d, -448.f), 448.f);
;     int w = __builtin_amdgcn_cvt_pk_fp8_f32(a, b, 0, false); w = __builtin_amdgcn_cvt_pk_fp8_f32(c, d, w, true); return (unsigned)w; }
;     ...
; #pragma unroll
;     for (int i = 0; i < 32; ++i) v[i] = sc >= 0 ? W[(size_t)(k0 + 2 * i + (lane >> 5)) * Nsrc + sc] : 0.f;
; #pragma unroll
;     for (int i = 0; i < 32; ++i) { const int k = k0 + 2 * i + (lane >> 5); float x = v[i] * wscale; if (KS) x *= (k < ksplit ? ksA[k] : ksB[k - ksplit]); scr[(2 * i + (lane >> 5)) * 33 + (lane & 31)] = x; }
;     LDS_WAIT(); asm volatile("" ::: "memory");
;     const int c = lane & 7;
; #pragma unroll
;     for (int j = 0; j < 4; ++j) { const int n = (lane >> 3) + 8 * j; const LAS float* s = scr + (8 * c) * 33 + n;
;         const unsigned long long o = (unsigned long long)pg8::pk4_fp8(s[0 * 33], s[1 * 33], s[2 * 33], s[3 * 33]) | ((unsigned long long)pg8::pk4_fp8(s[4 * 33], s[5 * 33], s[6 * 33], s[7 * 33]) << 32);
;         *(GAS unsigned long long*)(WT + (size_t)(n0 + n) * K + k0 + 8 * c) = o; }
;     LDS_WAIT(); asm volatile("" ::: "memory");
	s_add_u32 s8, s34, 0xa000
	s_addc_u32 s9, s35, 0
	global_load_dwordx4 v[144:147], v74, s[8:9]
	s_add_u32 s8, s8, 0x20000
	s_addc_u32 s9, s9, 0
	global_load_dwordx4 v[148:151], v74, s[8:9]
	s_add_u32 s8, s8, 0x20000
	s_addc_u32 s9, s9, 0
	global_load_dwordx4 v[152:155], v74, s[8:9]
	s_add_u32 s8, s8, 0x20000
	s_addc_u32 s9, s9, 0
	global_load_dwordx4 v[156:159], v74, s[8:9]
	s_add_u32 s8, s8, 0x20000
	s_addc_u32 s9, s9, 0
	global_load_dwordx4 v[160:163], v74, s[8:9]
	s_add_u32 s8, s8, 0x20000
	s_addc_u32 s9, s9, 0
	global_load_dwordx4 v[164:167], v74, s[8:9]
	s_add_u32 s8, s8, 0x20000
	s_addc_u32 s9, s9, 0
	global_load_dwordx4 v[168:171], v74, s[8:9]
	s_add_u32 s8, s8, 0x20000
	s_addc_u32 s9, s9, 0
	global_load_dwordx4 v[172:175], v74, s[8:9]
	s_add_u32 s6, s36, 0x2000000
	s_addc_u32 s7, s37, 0
	ds_read_b32 v226, v211
	ds_read_b32 v227, v211 offset:512
	ds_read_b32 v228, v211 offset:1024
	ds_read_b32 v229, v211 offset:1536
	ds_read_b32 v230, v211 offset:2048
	ds_read_b32 v231, v211 offset:2560
	ds_read_b32 v232, v211 offset:3072
	ds_read_b32 v233, v211 offset:3584
	ds_read_b32 v234, v211 offset:4096
	ds_read_b32 v235, v211 offset:4608
	ds_read_b32 v236, v211 offset:5120
	ds_read_b32 v237, v211 offset:5632
	ds_read_b32 v238, v211 offset:6144
	ds_read_b32 v239, v211 offset:6656
	ds_read_b32 v240, v211 offset:7168
	ds_read_b32 v241, v211 offset:7680
	s_waitcnt lgkmcnt(0)
	v_max_f32_e32 v226, v226, v226
	v_max_f32_e32 v227, v227, v227
	v_max_f32_e32 v228, v228, v228
	v_max_f32_e32 v229, v229, v229
	v_max_f32_e32 v230, v230, v230
	v_max_f32_e32 v231, v231, v231
	v_max_f32_e32 v232, v232, v232
	v_max_f32_e32 v233, v233, v233
	v_max_f32_e32 v234, v234, v234
	v_max_f32_e32 v235, v235, v235
	v_max_f32_e32 v236, v236, v236
	v_max_f32_e32 v237, v237, v237
	v_max_f32_e32 v238, v238, v238
	v_max_f32_e32 v239, v239, v239
	v_max_f32_e32 v240, v240, v240
	v_max_f32_e32 v241, v241, v241
	v_med3_f32 v226, v226, s62, v95
	v_med3_f32 v227, v227, s62, v95
	v_med3_f32 v228, v228, s62, v95
	v_med3_f32 v229, v229, s62, v95
	v_med3_f32 v230, v230, s62, v95
	v_med3_f32 v231, v231, s62, v95
	v_med3_f32 v232, v232, s62, v95
	v_med3_f32 v233, v233, s62, v95
	v_med3_f32 v234, v234, s62, v95
	v_med3_f32 v235, v235, s62, v95
	v_med3_f32 v236, v236, s62, v95
	v_med3_f32 v237, v237, s62, v95
	v_med3_f32 v238, v238, s62, v95
	v_med3_f32 v239, v239, s62, v95
	v_med3_f32 v240, v240, s62, v95
	v_med3_f32 v241, v241, s62, v95
	v_mov_b32_e32 v242, 0
	v_mov_b32_e32 v243, 0
	v_mov_b32_e32 v244, 0
	v_mov_b32_e32 v245, 0
	v_cvt_pk_fp8_f32 v242, v226, v227
	v_cvt_pk_fp8_f32 v243, v230, v231
	v_cvt_pk_fp8_f32 v244, v234, v235
	v_cvt_pk_fp8_f32 v245, v238, v239
	v_cvt_pk_fp8_f32 v242, v228, v229 op_sel:[0,0,1]
	v_cvt_pk_fp8_f32 v243, v232, v233 op_sel:[0,0,1]
	v_cvt_pk_fp8_f32 v244, v236, v237 op_sel:[0,0,1]
	v_cvt_pk_fp8_f32 v245, v240, v241 op_sel:[0,0,1]
	s_nop 0
	global_store_dwordx4 v77, v[242:245], s[6:7]
	ds_read_b32 v226, v213
	ds_read_b32 v227, v213 offset:512
	ds_read_b32 v228, v213 offset:1024
	ds_read_b32 v229, v213 offset:1536
	ds_read_b32 v230, v213 offset:2048
	ds_read_b32 v231, v213 offset:2560
	ds_read_b32 v232, v213 offset:3072
	ds_read_b32 v233, v213 offset:3584
	ds_read_b32 v234, v213 offset:4096
	ds_read_b32 v235, v213 offset:4608
	ds_read_b32 v236, v213 offset:5120
	ds_read_b32 v237, v213 offset:5632
	ds_read_b32 v238, v213 offset:6144
	ds_read_b32 v239, v213 offset:6656
	ds_read_b32 v240, v213 offset:7168
	ds_read_b32 v241, v213 offset:7680
	s_waitcnt lgkmcnt(0)
	v_max_f32_e32 v226, v226, v226
	v_max_f32_e32 v227, v227, v227
	v_max_f32_e32 v228, v228, v228
	v_max_f32_e32 v229, v229, v229
	v_max_f32_e32 v230, v230, v230
	v_max_f32_e32 v231, v231, v231
	v_max_f32_e32 v232, v232, v232
	v_max_f32_e32 v233, v233, v233
	v_max_f32_e32 v234, v234, v234
	v_max_f32_e32 v235, v235, v235
	v_max_f32_e32 v236, v236, v236
	v_max_f32_e32 v237, v237, v237
	v_max_f32_e32 v238, v238, v238
	v_max_f32_e32 v239, v239, v239
	v_max_f32_e32 v240, v240, v240
	v_max_f32_e32 v241, v241, v241
	v_med3_f32 v226, v226, s62, v95
	v_med3_f32 v227, v227, s62, v95
	v_med3_f32 v228, v228, s62, v95
	v_med3_f32 v229, v229, s62, v95
	v_med3_f32 v230, v230, s62, v95
	v_med3_f32 v231, v231, s62, v95
	v_med3_f32 v232, v232, s62, v95
	v_med3_f32 v233, v233, s62, v95
	v_med3_f32 v234, v234, s62, v95
	v_med3_f32 v235, v235, s62, v95
	v_med3_f32 v236, v236, s62, v95
	v_med3_f32 v237, v237, s62, v95
	v_med3_f32 v238, v238, s62, v95
	v_med3_f32 v239, v239, s62, v95
	v_med3_f32 v240, v240, s62, v95
	v_med3_f32 v241, v241, s62, v95
	v_mov_b32_e32 v242, 0
	v_mov_b32_e32 v243, 0
	v_mov_b32_e32 v244, 0
	v_mov_b32_e32 v245, 0
	v_cvt_pk_fp8_f32 v242, v226, v227
	v_cvt_pk_fp8_f32 v243, v230, v231
	v_cvt_pk_fp8_f32 v244, v234, v235
	v_cvt_pk_fp8_f32 v245, v238, v239
	v_cvt_pk_fp8_f32 v242, v228, v229 op_sel:[0,0,1]
	v_cvt_pk_fp8_f32 v243, v232, v233 op_sel:[0,0,1]
	v_cvt_pk_fp8_f32 v244, v236, v237 op_sel:[0,0,1]
	v_cvt_pk_fp8_f32 v245, v240, v241 op_sel:[0,0,1]
	s_nop 0
	global_store_dwordx4 v78, v[242:245], s[6:7]
	s_waitcnt vmcnt(12)
	v_mul_f32_e32 v176, v34, v176
	v_mul_f32_e32 v177, v34, v177
	v_mul_f32_e32 v178, v34, v178
	v_mul_f32_e32 v179, v34, v179
	ds_write_b128 v210, v[176:179]
	v_mul_f32_e32 v180, v35, v180
	v_mul_f32_e32 v181, v35, v181
	v_mul_f32_e32 v182, v35, v182
	v_mul_f32_e32 v183, v35, v183
	ds_write_b128 v210, v[180:183] offset:1024
	v_mul_f32_e32 v184, v36, v184
	v_mul_f32_e32 v185, v36, v185
	v_mul_f32_e32 v186, v36, v186
	v_mul_f32_e32 v187, v36, v187
	ds_write_b128 v210, v[184:187] offset:2048
	v_mul_f32_e32 v188, v37, v188
	v_mul_f32_e32 v189, v37, v189
	v_mul_f32_e32 v190, v37, v190
	v_mul_f32_e32 v191, v37, v191
	ds_write_b128 v210, v[188:191] offset:3072
	v_mul_f32_e32 v192, v38, v192
	v_mul_f32_e32 v193, v38, v193
	v_mul_f32_e32 v194, v38, v194
	v_mul_f32_e32 v195, v38, v195
	ds_write_b128 v210, v[192:195] offset:4096
	v_mul_f32_e32 v196, v39, v196
	v_mul_f32_e32 v197, v39, v197
	v_mul_f32_e32 v198, v39, v198
	v_mul_f32_e32 v199, v39, v199
	ds_write_b128 v210, v[196:199] offset:5120
	v_mul_f32_e32 v200, v40, v200
	v_mul_f32_e32 v201, v40, v201
	v_mul_f32_e32 v202, v40, v202
	v_mul_f32_e32 v203, v40, v203
	ds_write_b128 v210, v[200:203] offset:6144
	v_mul_f32_e32 v204, v41, v204
	v_mul_f32_e32 v205, v41, v205
	v_mul_f32_e32 v206, v41, v206
	v_mul_f32_e32 v207, v41, v207
	ds_write_b128 v210, v[204:207] offset:7168
	s_waitcnt lgkmcnt(0)
	s_barrier
; #define GAS __attribute__((address_space(1)))
; #define LAS __attribute__((address_space(3)))
; #define LDS_WAIT() asm volatile("s_waitcnt lgkmcnt(0)" ::: "memory")
; __device__ __forceinline__ unsigned pk4_fp8(float a, float b, float c, float d) {
;     a = fminf(fmaxf(a, -448.f), 448.f); b = fminf(fmaxf(b, -448.f), 448.f); c = fminf(fmaxf(c, -448.f), 448.f); d = fminf(fmaxf(d, -448.f), 448.f);
;     int w = __builtin_amdgcn_cvt_pk_fp8_f32(a, b, 0, false); w = __builtin_amdgcn_cvt_pk_fp8_f32(c, d, w, true); return (unsigned)w; }
;     ...
; #pragma unroll
;     for (int i = 0; i < 32; ++i) v[i] = sc >= 0 ? W[(size_t)(k0 + 2 * i + (lane >> 5)) * Nsrc + sc] : 0.f;
; #pragma unroll
;     for (int i = 0; i < 32; ++i) { const int k = k0 + 2 * i + (lane >> 5); float x = v[i] * wscale; if (KS) x *= (k < ksplit ? ksA[k] : ksB[k - ksplit]); scr[(2 * i + (lane >> 5)) * 33 + (lane & 31)] = x; }
;     LDS_WAIT(); asm volatile("" ::: "memory");
;     const int c = lane & 7;
; #pragma unroll
;     for (int j = 0; j < 4; ++j) { const int n = (lane >> 3) + 8 * j; const LAS float* s = scr + (8 * c) * 33 + n;
;         const unsigned long long o = (unsigned long long)pg8::pk4_fp8(s[0 * 33], s[1 * 33], s[2 * 33], s[3 * 33]) | ((unsigned long long)pg8::pk4_fp8(s[4 * 33], s[5 * 33], s[6 * 33], s[7 * 33]) << 32);
;         *(GAS unsigned long long*)(WT + (size_t)(n0 + n) * K + k0 + 8 * c) = o; }
;     LDS_WAIT(); asm volatile("" ::: "memory");
	s_add_u32 s8, s34, 0xb000
	s_addc_u32 s9, s35, 0
	global_load_dwordx4 v[176:179], v74, s[8:9]
	s_add_u32 s8, s8, 0x20000
	s_addc_u32 s9, s9, 0
	global_load_dwordx4 v[180:183], v74, s[8:9]
	s_add_u32 s8, s8, 0x20000
	s_addc_u32 s9, s9, 0
	global_load_dwordx4 v[184:187], v74, s[8:9]
	s_add_u32 s8, s8, 0x20000
	s_addc_u32 s9, s9, 0
	global_load_dwordx4 v[188:191], v74, s[8:9]
	s_add_u32 s8, s8, 0x20000
	s_addc_u32 s9, s9, 0
	global_load_dwordx4 v[192:195], v74, s[8:9]
	s_add_u32 s8, s8, 0x20000
	s_addc_u32 s9, s9, 0
	global_load_dwordx4 v[196:199], v74, s[8:9]
	s_add_u32 s8, s8, 0x20000
	s_addc_u32 s9, s9, 0
	global_load_dwordx4 v[200:203], v74, s[8:9]
	s_add_u32 s8, s8, 0x20000
	s_addc_u32 s9, s9, 0
	global_load_dwordx4 v[204:207], v74, s[8:9]
	s_add_u32 s6, s36, 0x2400000
	s_addc_u32 s7, s37, 0
	ds_read_b32 v226, v212
	ds_read_b32 v227, v212 offset:512
	ds_read_b32 v228, v212 offset:1024
	ds_read_b32 v229, v212 offset:1536
	ds_read_b32 v230, v212 offset:2048
	ds_read_b32 v231, v212 offset:2560
	ds_read_b32 v232, v212 offset:3072
	ds_read_b32 v233, v212 offset:3584
	ds_read_b32 v234, v212 offset:4096
	ds_read_b32 v235, v212 offset:4608
	ds_read_b32 v236, v212 offset:5120
	ds_read_b32 v237, v212 offset:5632
	ds_read_b32 v238, v212 offset:6144
	ds_read_b32 v239, v212 offset:6656
	ds_read_b32 v240, v212 offset:7168
	ds_read_b32 v241, v212 offset:7680
	s_waitcnt lgkmcnt(0)
	v_max_f32_e32 v226, v226, v226
	v_max_f32_e32 v227, v227, v227
	v_max_f32_e32 v228, v228, v228
	v_max_f32_e32 v229, v229, v229
	v_max_f32_e32 v230, v230, v230
	v_max_f32_e32 v231, v231, v231
	v_max_f32_e32 v232, v232, v232
	v_max_f32_e32 v233, v233, v233
	v_max_f32_e32 v234, v234, v234
	v_max_f32_e32 v235, v235, v235
	v_max_f32_e32 v236, v236, v236
	v_max_f32_e32 v237, v237, v237
	v_max_f32_e32 v238, v238, v238
	v_max_f32_e32 v239, v239, v239
	v_max_f32_e32 v240, v240, v240
	v_max_f32_e32 v241, v241, v241
	v_med3_f32 v226, v226, s62, v95
	v_med3_f32 v227, v227, s62, v95
	v_med3_f32 v228, v228, s62, v95
	v_med3_f32 v229, v229, s62, v95
	v_med3_f32 v230, v230, s62, v95
	v_med3_f32 v231, v231, s62, v95
	v_med3_f32 v232, v232, s62, v95
	v_med3_f32 v233, v233, s62, v95
	v_med3_f32 v234, v234, s62, v95
	v_med3_f32 v235, v235, s62, v95
	v_med3_f32 v236, v236, s62, v95
	v_med3_f32 v237, v237, s62, v95
	v_med3_f32 v238, v238, s62, v95
	v_med3_f32 v239, v239, s62, v95
	v_med3_f32 v240, v240, s62, v95
	v_med3_f32 v241, v241, s62, v95
	v_mov_b32_e32 v242, 0
	v_mov_b32_e32 v243, 0
	v_mov_b32_e32 v244, 0
	v_mov_b32_e32 v245, 0
	v_cvt_pk_fp8_f32 v242, v226, v227
	v_cvt_pk_fp8_f32 v243, v230, v231
	v_cvt_pk_fp8_f32 v244, v234, v235
	v_cvt_pk_fp8_f32 v245, v238, v239
	v_cvt_pk_fp8_f32 v242, v228, v229 op_sel:[0,0,1]
	v_cvt_pk_fp8_f32 v243, v232, v233 op_sel:[0,0,1]
	v_cvt_pk_fp8_f32 v244, v236, v237 op_sel:[0,0,1]
	v_cvt_pk_fp8_f32 v245, v240, v241 op_sel:[0,0,1]
	s_nop 0
	global_store_dwordx4 v77, v[242:245], s[6:7]
	ds_read_b32 v226, v214
	ds_read_b32 v227, v214 offset:512
	ds_read_b32 v228, v214 offset:1024
	ds_read_b32 v229, v214 offset:1536
	ds_read_b32 v230, v214 offset:2048
	ds_read_b32 v231, v214 offset:2560
	ds_read_b32 v232, v214 offset:3072
	ds_read_b32 v233, v214 offset:3584
	ds_read_b32 v234, v214 offset:4096
	ds_read_b32 v235, v214 offset:4608
	ds_read_b32 v236, v214 offset:5120
	ds_read_b32 v237, v214 offset:5632
	ds_read_b32 v238, v214 offset:6144
	ds_read_b32 v239, v214 offset:6656
	ds_read_b32 v240, v214 offset:7168
	ds_read_b32 v241, v214 offset:7680
	s_waitcnt lgkmcnt(0)
	v_max_f32_e32 v226, v226, v226
	v_max_f32_e32 v227, v227, v227
	v_max_f32_e32 v228, v228, v228
	v_max_f32_e32 v229, v229, v229
	v_max_f32_e32 v230, v230, v230
	v_max_f32_e32 v231, v231, v231
	v_max_f32_e32 v232, v232, v232
	v_max_f32_e32 v233, v233, v233
	v_max_f32_e32 v234, v234, v234
	v_max_f32_e32 v235, v235, v235
	v_max_f32_e32 v236, v236, v236
	v_max_f32_e32 v237, v237, v237
	v_max_f32_e32 v238, v238, v238
	v_max_f32_e32 v239, v239, v239
	v_max_f32_e32 v240, v240, v240
	v_max_f32_e32 v241, v241, v241
	v_med3_f32 v226, v226, s62, v95
	v_med3_f32 v227, v227, s62, v95
	v_med3_f32 v228, v228, s62, v95
	v_med3_f32 v229, v229, s62, v95
	v_med3_f32 v230, v230, s62, v95
	v_med3_f32 v231, v231, s62, v95
	v_med3_f32 v232, v232, s62, v95
	v_med3_f32 v233, v233, s62, v95
	v_med3_f32 v234, v234, s62, v95
	v_med3_f32 v235, v235, s62, v95
	v_med3_f32 v236, v236, s62, v95
	v_med3_f32 v237, v237, s62, v95
	v_med3_f32 v238, v238, s62, v95
	v_med3_f32 v239, v239, s62, v95
	v_med3_f32 v240, v240, s62, v95
	v_med3_f32 v241, v241, s62, v95
	v_mov_b32_e32 v242, 0
	v_mov_b32_e32 v243, 0
	v_mov_b32_e32 v244, 0
	v_mov_b32_e32 v245, 0
	v_cvt_pk_fp8_f32 v242, v226, v227
	v_cvt_pk_fp8_f32 v243, v230, v231
	v_cvt_pk_fp8_f32 v244, v234, v235
	v_cvt_pk_fp8_f32 v245, v238, v239
	v_cvt_pk_fp8_f32 v242, v228, v229 op_sel:[0,0,1]
	v_cvt_pk_fp8_f32 v243, v232, v233 op_sel:[0,0,1]
	v_cvt_pk_fp8_f32 v244, v236, v237 op_sel:[0,0,1]
	v_cvt_pk_fp8_f32 v245, v240, v241 op_sel:[0,0,1]
	s_nop 0
	global_store_dwordx4 v78, v[242:245], s[6:7]
	s_waitcnt vmcnt(12)
	v_mul_f32_e32 v144, v34, v144
	v_mul_f32_e32 v145, v34, v145
	v_mul_f32_e32 v146, v34, v146
	v_mul_f32_e32 v147, v34, v147
	ds_write_b128 v209, v[144:147]
	v_mul_f32_e32 v148, v35, v148
	v_mul_f32_e32 v149, v35, v149
	v_mul_f32_e32 v150, v35, v150
	v_mul_f32_e32 v151, v35, v151
	ds_write_b128 v209, v[148:151] offset:1024
	v_mul_f32_e32 v152, v36, v152
	v_mul_f32_e32 v153, v36, v153
	v_mul_f32_e32 v154, v36, v154
	v_mul_f32_e32 v155, v36, v155
	ds_write_b128 v209, v[152:155] offset:2048
	v_mul_f32_e32 v156, v37, v156
	v_mul_f32_e32 v157, v37, v157
	v_mul_f32_e32 v158, v37, v158
	v_mul_f32_e32 v159, v37, v159
	ds_write_b128 v209, v[156:159] offset:3072
	v_mul_f32_e32 v160, v38, v160
	v_mul_f32_e32 v161, v38, v161
	v_mul_f32_e32 v162, v38, v162
	v_mul_f32_e32 v163, v38, v163
	ds_write_b128 v209, v[160:163] offset:4096
	v_mul_f32_e32 v164, v39, v164
	v_mul_f32_e32 v165, v39, v165
	v_mul_f32_e32 v166, v39, v166
	v_mul_f32_e32 v167, v39, v167
	ds_write_b128 v209, v[164:167] offset:5120
	v_mul_f32_e32 v168, v40, v168
	v_mul_f32_e32 v169, v40, v169
	v_mul_f32_e32 v170, v40, v170
	v_mul_f32_e32 v171, v40, v171
	ds_write_b128 v209, v[168:171] offset:6144
	v_mul_f32_e32 v172, v41, v172
	v_mul_f32_e32 v173, v41, v173
	v_mul_f32_e32 v174, v41, v174
	v_mul_f32_e32 v175, v41, v175
	ds_write_b128 v209, v[172:175] offset:7168
	s_waitcnt lgkmcnt(0)
	s_barrier
; #define GAS __attribute__((address_space(1)))
; #define LAS __attribute__((address_space(3)))
; #define LDS_WAIT() asm volatile("s_waitcnt lgkmcnt(0)" ::: "memory")
; __device__ __forceinline__ unsigned pk4_fp8(float a, float b, float c, float d) {
;     a = fminf(fmaxf(a, -448.f), 448.f); b = fminf(fmaxf(b, -448.f), 448.f); c = fminf(fmaxf(c, -448.f), 448.f); d = fminf(fmaxf(d, -448.f), 448.f);
;     int w = __builtin_amdgcn_cvt_pk_fp8_f32(a, b, 0, false); w = __builtin_amdgcn_cvt_pk_fp8_f32(c, d, w, true); return (unsigned)w; }
;     ...
; #pragma unroll
;     for (int i = 0; i < 32; ++i) v[i] = sc >= 0 ? W[(size_t)(k0 + 2 * i + (lane >> 5)) * Nsrc + sc] : 0.f;
; #pragma unroll
;     for (int i = 0; i < 32; ++i) { const int k = k0 + 2 * i + (lane >> 5); float x = v[i] * wscale; if (KS) x *= (k < ksplit ? ksA[k] : ksB[k - ksplit]); scr[(2 * i + (lane >> 5)) * 33 + (lane & 31)] = x; }
;     LDS_WAIT(); asm volatile("" ::: "memory");
;     const int c = lane & 7;
; #pragma unroll
;     for (int j = 0; j < 4; ++j) { const int n = (lane >> 3) + 8 * j; const LAS float* s = scr + (8 * c) * 33 + n;
;         const unsigned long long o = (unsigned long long)pg8::pk4_fp8(s[0 * 33], s[1 * 33], s[2 * 33], s[3 * 33]) | ((unsigned long long)pg8::pk4_fp8(s[4 * 33], s[5 * 33], s[6 * 33], s[7 * 33]) << 32);
;         *(GAS unsigned long long*)(WT + (size_t)(n0 + n) * K + k0 + 8 * c) = o; }
;     LDS_WAIT(); asm volatile("" ::: "memory");
	s_mov_b64 s[8:9], s[38:39]
	global_load_dwordx4 v[144:147], v75, s[8:9]
	s_add_u32 s8, s8, 0x8000
	s_addc_u32 s9, s9, 0
	global_load_dwordx4 v[148:151], v75, s[8:9]
	s_add_u32 s8, s8, 0x8000
	s_addc_u32 s9, s9, 0
	global_load_dwordx4 v[152:155], v75, s[8:9]
	s_add_u32 s8, s8, 0x8000
	s_addc_u32 s9, s9, 0
	global_load_dwordx4 v[156:159], v75, s[8:9]
	s_add_u32 s8, s8, 0x8000
	s_addc_u32 s9, s9, 0
	global_load_dwordx4 v[160:163], v75, s[8:9]
	s_add_u32 s8, s8, 0x8000
	s_addc_u32 s9, s9, 0
	global_load_dwordx4 v[164:167], v75, s[8:9]
	s_add_u32 s8, s8, 0x8000
	s_addc_u32 s9, s9, 0
	global_load_dwordx4 v[168:171], v75, s[8:9]
	s_add_u32 s8, s8, 0x8000
	s_addc_u32 s9, s9, 0
	global_load_dwordx4 v[172:175], v75, s[8:9]
	s_add_u32 s6, s36, 0x2800000
	s_addc_u32 s7, s37, 0
	ds_read_b32 v226, v211
	ds_read_b32 v227, v211 offset:512
	ds_read_b32 v228, v211 offset:1024
	ds_read_b32 v229, v211 offset:1536
	ds_read_b32 v230, v211 offset:2048
	ds_read_b32 v231, v211 offset:2560
	ds_read_b32 v232, v211 offset:3072
	ds_read_b32 v233, v211 offset:3584
	ds_read_b32 v234, v211 offset:4096
	ds_read_b32 v235, v211 offset:4608
	ds_read_b32 v236, v211 offset:5120
	ds_read_b32 v237, v211 offset:5632
	ds_read_b32 v238, v211 offset:6144
	ds_read_b32 v239, v211 offset:6656
	ds_read_b32 v240, v211 offset:7168
	ds_read_b32 v241, v211 offset:7680
	s_waitcnt lgkmcnt(0)
	v_max_f32_e32 v226, v226, v226
	v_max_f32_e32 v227, v227, v227
	v_max_f32_e32 v228, v228, v228
	v_max_f32_e32 v229, v229, v229
	v_max_f32_e32 v230, v230, v230
	v_max_f32_e32 v231, v231, v231
	v_max_f32_e32 v232, v232, v232
	v_max_f32_e32 v233, v233, v233
	v_max_f32_e32 v234, v234, v234
	v_max_f32_e32 v235, v235, v235
	v_max_f32_e32 v236, v236, v236
	v_max_f32_e32 v237, v237, v237
	v_max_f32_e32 v238, v238, v238
	v_max_f32_e32 v239, v239, v239
	v_max_f32_e32 v240, v240, v240
	v_max_f32_e32 v241, v241, v241
	v_med3_f32 v226, v226, s62, v95
	v_med3_f32 v227, v227, s62, v95
	v_med3_f32 v228, v228, s62, v95
	v_med3_f32 v229, v229, s62, v95
	v_med3_f32 v230, v230, s62, v95
	v_med3_f32 v231, v231, s62, v95
	v_med3_f32 v232, v232, s62, v95
	v_med3_f32 v233, v233, s62, v95
	v_med3_f32 v234, v234, s62, v95
	v_med3_f32 v235, v235, s62, v95
	v_med3_f32 v236, v236, s62, v95
	v_med3_f32 v237, v237, s62, v95
	v_med3_f32 v238, v238, s62, v95
	v_med3_f32 v239, v239, s62, v95
	v_med3_f32 v240, v240, s62, v95
	v_med3_f32 v241, v241, s62, v95
	v_mov_b32_e32 v242, 0
	v_mov_b32_e32 v243, 0
	v_mov_b32_e32 v244, 0
	v_mov_b32_e32 v245, 0
	v_cvt_pk_fp8_f32 v242, v226, v227
	v_cvt_pk_fp8_f32 v243, v230, v231
	v_cvt_pk_fp8_f32 v244, v234, v235
	v_cvt_pk_fp8_f32 v245, v238, v239
	v_cvt_pk_fp8_f32 v242, v228, v229 op_sel:[0,0,1]
	v_cvt_pk_fp8_f32 v243, v232, v233 op_sel:[0,0,1]
	v_cvt_pk_fp8_f32 v244, v236, v237 op_sel:[0,0,1]
	v_cvt_pk_fp8_f32 v245, v240, v241 op_sel:[0,0,1]
	s_nop 0
	global_store_dwordx4 v77, v[242:245], s[6:7]
	ds_read_b32 v226, v213
	ds_read_b32 v227, v213 offset:512
	ds_read_b32 v228, v213 offset:1024
	ds_read_b32 v229, v213 offset:1536
	ds_read_b32 v230, v213 offset:2048
	ds_read_b32 v231, v213 offset:2560
	ds_read_b32 v232, v213 offset:3072
	ds_read_b32 v233, v213 offset:3584
	ds_read_b32 v234, v213 offset:4096
	ds_read_b32 v235, v213 offset:4608
	ds_read_b32 v236, v213 offset:5120
	ds_read_b32 v237, v213 offset:5632
	ds_read_b32 v238, v213 offset:6144
	ds_read_b32 v239, v213 offset:6656
	ds_read_b32 v240, v213 offset:7168
	ds_read_b32 v241, v213 offset:7680
	s_waitcnt lgkmcnt(0)
	v_max_f32_e32 v226, v226, v226
	v_max_f32_e32 v227, v227, v227
	v_max_f32_e32 v228, v228, v228
	v_max_f32_e32 v229, v229, v229
	v_max_f32_e32 v230, v230, v230
	v_max_f32_e32 v231, v231, v231
	v_max_f32_e32 v232, v232, v232
	v_max_f32_e32 v233, v233, v233
	v_max_f32_e32 v234, v234, v234
	v_max_f32_e32 v235, v235, v235
	v_max_f32_e32 v236, v236, v236
	v_max_f32_e32 v237, v237, v237
	v_max_f32_e32 v238, v238, v238
	v_max_f32_e32 v239, v239, v239
	v_max_f32_e32 v240, v240, v240
	v_max_f32_e32 v241, v241, v241
	v_med3_f32 v226, v226, s62, v95
	v_med3_f32 v227, v227, s62, v95
	v_med3_f32 v228, v228, s62, v95
	v_med3_f32 v229, v229, s62, v95
	v_med3_f32 v230, v230, s62, v95
	v_med3_f32 v231, v231, s62, v95
	v_med3_f32 v232, v232, s62, v95
	v_med3_f32 v233, v233, s62, v95
	v_med3_f32 v234, v234, s62, v95
	v_med3_f32 v235, v235, s62, v95
	v_med3_f32 v236, v236, s62, v95
	v_med3_f32 v237, v237, s62, v95
	v_med3_f32 v238, v238, s62, v95
	v_med3_f32 v239, v239, s62, v95
	v_med3_f32 v240, v240, s62, v95
	v_med3_f32 v241, v241, s62, v95
	v_mov_b32_e32 v242, 0
	v_mov_b32_e32 v243, 0
	v_mov_b32_e32 v244, 0
	v_mov_b32_e32 v245, 0
	v_cvt_pk_fp8_f32 v242, v226, v227
	v_cvt_pk_fp8_f32 v243, v230, v231
	v_cvt_pk_fp8_f32 v244, v234, v235
	v_cvt_pk_fp8_f32 v245, v238, v239
	v_cvt_pk_fp8_f32 v242, v228, v229 op_sel:[0,0,1]
	v_cvt_pk_fp8_f32 v243, v232, v233 op_sel:[0,0,1]
	v_cvt_pk_fp8_f32 v244, v236, v237 op_sel:[0,0,1]
	v_cvt_pk_fp8_f32 v245, v240, v241 op_sel:[0,0,1]
	s_nop 0
	global_store_dwordx4 v78, v[242:245], s[6:7]
	s_waitcnt vmcnt(12)
	v_mul_f32_e32 v176, v34, v176
	v_mul_f32_e32 v177, v34, v177
	v_mul_f32_e32 v178, v34, v178
	v_mul_f32_e32 v179, v34, v179
	ds_write_b128 v210, v[176:179]
	v_mul_f32_e32 v180, v35, v180
	v_mul_f32_e32 v181, v35, v181
	v_mul_f32_e32 v182, v35, v182
	v_mul_f32_e32 v183, v35, v183
	ds_write_b128 v210, v[180:183] offset:1024
	v_mul_f32_e32 v184, v36, v184
	v_mul_f32_e32 v185, v36, v185
	v_mul_f32_e32 v186, v36, v186
	v_mul_f32_e32 v187, v36, v187
	ds_write_b128 v210, v[184:187] offset:2048
	v_mul_f32_e32 v188, v37, v188
	v_mul_f32_e32 v189, v37, v189
	v_mul_f32_e32 v190, v37, v190
	v_mul_f32_e32 v191, v37, v191
	ds_write_b128 v210, v[188:191] offset:3072
	v_mul_f32_e32 v192, v38, v192
	v_mul_f32_e32 v193, v38, v193
	v_mul_f32_e32 v194, v38, v194
	v_mul_f32_e32 v195, v38, v195
	ds_write_b128 v210, v[192:195] offset:4096
	v_mul_f32_e32 v196, v39, v196
	v_mul_f32_e32 v197, v39, v197
	v_mul_f32_e32 v198, v39, v198
	v_mul_f32_e32 v199, v39, v199
	ds_write_b128 v210, v[196:199] offset:5120
	v_mul_f32_e32 v200, v40, v200
	v_mul_f32_e32 v201, v40, v201
	v_mul_f32_e32 v202, v40, v202
	v_mul_f32_e32 v203, v40, v203
	ds_write_b128 v210, v[200:203] offset:6144
	v_mul_f32_e32 v204, v41, v204
	v_mul_f32_e32 v205, v41, v205
	v_mul_f32_e32 v206, v41, v206
	v_mul_f32_e32 v207, v41, v207
	ds_write_b128 v210, v[204:207] offset:7168
	s_waitcnt lgkmcnt(0)
	s_barrier
; #define GAS __attribute__((address_space(1)))
; #define LAS __attribute__((address_space(3)))
; #define LDS_WAIT() asm volatile("s_waitcnt lgkmcnt(0)" ::: "memory")
; __device__ __forceinline__ unsigned pk4_fp8(float a, float b, float c, float d) {
;     a = fminf(fmaxf(a, -448.f), 448.f); b = fminf(fmaxf(b, -448.f), 448.f); c = fminf(fmaxf(c, -448.f), 448.f); d = fminf(fmaxf(d, -448.f), 448.f);
;     int w = __builtin_amdgcn_cvt_pk_fp8_f32(a, b, 0, false); w = __builtin_amdgcn_cvt_pk_fp8_f32(c, d, w, true); return (unsigned)w; }
;     ...
; #pragma unroll
;     for (int i = 0; i < 32; ++i) v[i] = sc >= 0 ? W[(size_t)(k0 + 2 * i + (lane >> 5)) * Nsrc + sc] : 0.f;
; #pragma unroll
;     for (int i = 0; i < 32; ++i) { const int k = k0 + 2 * i + (lane >> 5); float x = v[i] * wscale; if (KS) x *= (k < ksplit ? ksA[k] : ksB[k - ksplit]); scr[(2 * i + (lane >> 5)) * 33 + (lane & 31)] = x; }
;     LDS_WAIT(); asm volatile("" ::: "memory");
;     const int c = lane & 7;
; #pragma unroll
;     for (int j = 0; j < 4; ++j) { const int n = (lane >> 3) + 8 * j; const LAS float* s = scr + (8 * c) * 33 + n;
;         const unsigned long long o = (unsigned long long)pg8::pk4_fp8(s[0 * 33], s[1 * 33], s[2 * 33], s[3 * 33]) | ((unsigned long long)pg8::pk4_fp8(s[4 * 33], s[5 * 33], s[6 * 33], s[7 * 33]) << 32);
;         *(GAS unsigned long long*)(WT + (size_t)(n0 + n) * K + k0 + 8 * c) = o; }
;     LDS_WAIT(); asm volatile("" ::: "memory");
	s_add_u32 s8, s38, 0x1000
	s_addc_u32 s9, s39, 0
	global_load_dwordx4 v[176:179], v75, s[8:9]
	s_add_u32 s8, s8, 0x8000
	s_addc_u32 s9, s9, 0
	global_load_dwordx4 v[180:183], v75, s[8:9]
	s_add_u32 s8, s8, 0x8000
	s_addc_u32 s9, s9, 0
	global_load_dwordx4 v[184:187], v75, s[8:9]
	s_add_u32 s8, s8, 0x8000
	s_addc_u32 s9, s9, 0
	global_load_dwordx4 v[188:191], v75, s[8:9]
	s_add_u32 s8, s8, 0x8000
	s_addc_u32 s9, s9, 0
	global_load_dwordx4 v[192:195], v75, s[8:9]
	s_add_u32 s8, s8, 0x8000
	s_addc_u32 s9, s9, 0
	global_load_dwordx4 v[196:199], v75, s[8:9]
	s_add_u32 s8, s8, 0x8000
	s_addc_u32 s9, s9, 0
	global_load_dwordx4 v[200:203], v75, s[8:9]
	s_add_u32 s8, s8, 0x8000
	s_addc_u32 s9, s9, 0
	global_load_dwordx4 v[204:207], v75, s[8:9]
	s_add_u32 s6, s36, 0x2c00000
	s_addc_u32 s7, s37, 0
	ds_read_b32 v226, v212
	ds_read_b32 v227, v212 offset:512
	ds_read_b32 v228, v212 offset:1024
	ds_read_b32 v229, v212 offset:1536
	ds_read_b32 v230, v212 offset:2048
	ds_read_b32 v231, v212 offset:2560
	ds_read_b32 v232, v212 offset:3072
	ds_read_b32 v233, v212 offset:3584
	ds_read_b32 v234, v212 offset:4096
	ds_read_b32 v235, v212 offset:4608
	ds_read_b32 v236, v212 offset:5120
	ds_read_b32 v237, v212 offset:5632
	ds_read_b32 v238, v212 offset:6144
	ds_read_b32 v239, v212 offset:6656
	ds_read_b32 v240, v212 offset:7168
	ds_read_b32 v241, v212 offset:7680
	s_waitcnt lgkmcnt(0)
	v_max_f32_e32 v226, v226, v226
	v_max_f32_e32 v227, v227, v227
	v_max_f32_e32 v228, v228, v228
	v_max_f32_e32 v229, v229, v229
	v_max_f32_e32 v230, v230, v230
	v_max_f32_e32 v231, v231, v231
	v_max_f32_e32 v232, v232, v232
	v_max_f32_e32 v233, v233, v233
	v_max_f32_e32 v234, v234, v234
	v_max_f32_e32 v235, v235, v235
	v_max_f32_e32 v236, v236, v236
	v_max_f32_e32 v237, v237, v237
	v_max_f32_e32 v238, v238, v238
	v_max_f32_e32 v239, v239, v239
	v_max_f32_e32 v240, v240, v240
	v_max_f32_e32 v241, v241, v241
	v_med3_f32 v226, v226, s62, v95
	v_med3_f32 v227, v227, s62, v95
	v_med3_f32 v228, v228, s62, v95
	v_med3_f32 v229, v229, s62, v95
	v_med3_f32 v230, v230, s62, v95
	v_med3_f32 v231, v231, s62, v95
	v_med3_f32 v232, v232, s62, v95
	v_med3_f32 v233, v233, s62, v95
	v_med3_f32 v234, v234, s62, v95
	v_med3_f32 v235, v235, s62, v95
	v_med3_f32 v236, v236, s62, v95
	v_med3_f32 v237, v237, s62, v95
	v_med3_f32 v238, v238, s62, v95
	v_med3_f32 v239, v239, s62, v95
	v_med3_f32 v240, v240, s62, v95
	v_med3_f32 v241, v241, s62, v95
	v_mov_b32_e32 v242, 0
	v_mov_b32_e32 v243, 0
	v_mov_b32_e32 v244, 0
	v_mov_b32_e32 v245, 0
	v_cvt_pk_fp8_f32 v242, v226, v227
	v_cvt_pk_fp8_f32 v243, v230, v231
	v_cvt_pk_fp8_f32 v244, v234, v235
	v_cvt_pk_fp8_f32 v245, v238, v239
	v_cvt_pk_fp8_f32 v242, v228, v229 op_sel:[0,0,1]
	v_cvt_pk_fp8_f32 v243, v232, v233 op_sel:[0,0,1]
	v_cvt_pk_fp8_f32 v244, v236, v237 op_sel:[0,0,1]
	v_cvt_pk_fp8_f32 v245, v240, v241 op_sel:[0,0,1]
	s_nop 0
	global_store_dwordx4 v77, v[242:245], s[6:7]
	ds_read_b32 v226, v214
	ds_read_b32 v227, v214 offset:512
	ds_read_b32 v228, v214 offset:1024
	ds_read_b32 v229, v214 offset:1536
	ds_read_b32 v230, v214 offset:2048
	ds_read_b32 v231, v214 offset:2560
	ds_read_b32 v232, v214 offset:3072
	ds_read_b32 v233, v214 offset:3584
	ds_read_b32 v234, v214 offset:4096
	ds_read_b32 v235, v214 offset:4608
	ds_read_b32 v236, v214 offset:5120
	ds_read_b32 v237, v214 offset:5632
	ds_read_b32 v238, v214 offset:6144
	ds_read_b32 v239, v214 offset:6656
	ds_read_b32 v240, v214 offset:7168
	ds_read_b32 v241, v214 offset:7680
	s_waitcnt lgkmcnt(0)
	v_max_f32_e32 v226, v226, v226
	v_max_f32_e32 v227, v227, v227
	v_max_f32_e32 v228, v228, v228
	v_max_f32_e32 v229, v229, v229
	v_max_f32_e32 v230, v230, v230
	v_max_f32_e32 v231, v231, v231
	v_max_f32_e32 v232, v232, v232
	v_max_f32_e32 v233, v233, v233
	v_max_f32_e32 v234, v234, v234
	v_max_f32_e32 v235, v235, v235
	v_max_f32_e32 v236, v236, v236
	v_max_f32_e32 v237, v237, v237
	v_max_f32_e32 v238, v238, v238
	v_max_f32_e32 v239, v239, v239
	v_max_f32_e32 v240, v240, v240
	v_max_f32_e32 v241, v241, v241
	v_med3_f32 v226, v226, s62, v95
	v_med3_f32 v227, v227, s62, v95
	v_med3_f32 v228, v228, s62, v95
	v_med3_f32 v229, v229, s62, v95
	v_med3_f32 v230, v230, s62, v95
	v_med3_f32 v231, v231, s62, v95
	v_med3_f32 v232, v232, s62, v95
	v_med3_f32 v233, v233, s62, v95
	v_med3_f32 v234, v234, s62, v95
	v_med3_f32 v235, v235, s62, v95
	v_med3_f32 v236, v236, s62, v95
	v_med3_f32 v237, v237, s62, v95
	v_med3_f32 v238, v238, s62, v95
	v_med3_f32 v239, v239, s62, v95
	v_med3_f32 v240, v240, s62, v95
	v_med3_f32 v241, v241, s62, v95
	v_mov_b32_e32 v242, 0
	v_mov_b32_e32 v243, 0
	v_mov_b32_e32 v244, 0
	v_mov_b32_e32 v245, 0
	v_cvt_pk_fp8_f32 v242, v226, v227
	v_cvt_pk_fp8_f32 v243, v230, v231
	v_cvt_pk_fp8_f32 v244, v234, v235
	v_cvt_pk_fp8_f32 v245, v238, v239
	v_cvt_pk_fp8_f32 v242, v228, v229 op_sel:[0,0,1]
	v_cvt_pk_fp8_f32 v243, v232, v233 op_sel:[0,0,1]
	v_cvt_pk_fp8_f32 v244, v236, v237 op_sel:[0,0,1]
	v_cvt_pk_fp8_f32 v245, v240, v241 op_sel:[0,0,1]
	s_nop 0
	global_store_dwordx4 v78, v[242:245], s[6:7]
	s_waitcnt vmcnt(12)
	v_mul_f32_e32 v144, 0x43000000, v144
	v_mul_f32_e32 v145, 0x43000000, v145
	v_mul_f32_e32 v146, 0x43000000, v146
	v_mul_f32_e32 v147, 0x43000000, v147
	ds_write_b128 v209, v[144:147]
	v_mul_f32_e32 v148, 0x43000000, v148
	v_mul_f32_e32 v149, 0x43000000, v149
	v_mul_f32_e32 v150, 0x43000000, v150
	v_mul_f32_e32 v151, 0x43000000, v151
	ds_write_b128 v209, v[148:151] offset:1024
	v_mul_f32_e32 v152, 0x43000000, v152
	v_mul_f32_e32 v153, 0x43000000, v153
	v_mul_f32_e32 v154, 0x43000000, v154
	v_mul_f32_e32 v155, 0x43000000, v155
	ds_write_b128 v209, v[152:155] offset:2048
	v_mul_f32_e32 v156, 0x43000000, v156
	v_mul_f32_e32 v157, 0x43000000, v157
	v_mul_f32_e32 v158, 0x43000000, v158
	v_mul_f32_e32 v159, 0x43000000, v159
	ds_write_b128 v209, v[156:159] offset:3072
	v_mul_f32_e32 v160, 0x43000000, v160
	v_mul_f32_e32 v161, 0x43000000, v161
	v_mul_f32_e32 v162, 0x43000000, v162
	v_mul_f32_e32 v163, 0x43000000, v163
	ds_write_b128 v209, v[160:163] offset:4096
	v_mul_f32_e32 v164, 0x43000000, v164
	v_mul_f32_e32 v165, 0x43000000, v165
	v_mul_f32_e32 v166, 0x43000000, v166
	v_mul_f32_e32 v167, 0x43000000, v167
	ds_write_b128 v209, v[164:167] offset:5120
	v_mul_f32_e32 v168, 0x43000000, v168
	v_mul_f32_e32 v169, 0x43000000, v169
	v_mul_f32_e32 v170, 0x43000000, v170
	v_mul_f32_e32 v171, 0x43000000, v171
	ds_write_b128 v209, v[168:171] offset:6144
	v_mul_f32_e32 v172, 0x43000000, v172
	v_mul_f32_e32 v173, 0x43000000, v173
	v_mul_f32_e32 v174, 0x43000000, v174
	v_mul_f32_e32 v175, 0x43000000, v175
	ds_write_b128 v209, v[172:175] offset:7168
	s_waitcnt lgkmcnt(0)
	s_barrier
; #define GAS __attribute__((address_space(1)))
; #define LAS __attribute__((address_space(3)))
; #define LDS_WAIT() asm volatile("s_waitcnt lgkmcnt(0)" ::: "memory")
; __device__ __forceinline__ unsigned pk4_fp8(float a, float b, float c, float d) {
;     a = fminf(fmaxf(a, -448.f), 448.f); b = fminf(fmaxf(b, -448.f), 448.f); c = fminf(fmaxf(c, -448.f), 448.f); d = fminf(fmaxf(d, -448.f), 448.f);
;     int w = __builtin_amdgcn_cvt_pk_fp8_f32(a, b, 0, false); w = __builtin_amdgcn_cvt_pk_fp8_f32(c, d, w, true); return (unsigned)w; }
;     ...
; #pragma unroll
;     for (int i = 0; i < 32; ++i) v[i] = sc >= 0 ? W[(size_t)(k0 + 2 * i + (lane >> 5)) * Nsrc + sc] : 0.f;
; #pragma unroll
;     for (int i = 0; i < 32; ++i) { const int k = k0 + 2 * i + (lane >> 5); float x = v[i] * wscale; if (KS) x *= (k < ksplit ? ksA[k] : ksB[k - ksplit]); scr[(2 * i + (lane >> 5)) * 33 + (lane & 31)] = x; }
;     LDS_WAIT(); asm volatile("" ::: "memory");
;     const int c = lane & 7;
; #pragma unroll
;     for (int j = 0; j < 4; ++j) { const int n = (lane >> 3) + 8 * j; const LAS float* s = scr + (8 * c) * 33 + n;
;         const unsigned long long o = (unsigned long long)pg8::pk4_fp8(s[0 * 33], s[1 * 33], s[2 * 33], s[3 * 33]) | ((unsigned long long)pg8::pk4_fp8(s[4 * 33], s[5 * 33], s[6 * 33], s[7 * 33]) << 32);
;         *(GAS unsigned long long*)(WT + (size_t)(n0 + n) * K + k0 + 8 * c) = o; }
;     LDS_WAIT(); asm volatile("" ::: "memory");
	s_add_u32 s8, s38, 0x2000
	s_addc_u32 s9, s39, 0
	global_load_dwordx4 v[144:147], v75, s[8:9]
	s_add_u32 s8, s8, 0x8000
	s_addc_u32 s9, s9, 0
	global_load_dwordx4 v[148:151], v75, s[8:9]
	s_add_u32 s8, s8, 0x8000
	s_addc_u32 s9, s9, 0
	global_load_dwordx4 v[152:155], v75, s[8:9]
	s_add_u32 s8, s8, 0x8000
	s_addc_u32 s9, s9, 0
	global_load_dwordx4 v[156:159], v75, s[8:9]
	s_add_u32 s8, s8, 0x8000
	s_addc_u32 s9, s9, 0
	global_load_dwordx4 v[160:163], v75, s[8:9]
	s_add_u32 s8, s8, 0x8000
	s_addc_u32 s9, s9, 0
	global_load_dwordx4 v[164:167], v75, s[8:9]
	s_add_u32 s8, s8, 0x8000
	s_addc_u32 s9, s9, 0
	global_load_dwordx4 v[168:171], v75, s[8:9]
	s_add_u32 s8, s8, 0x8000
	s_addc_u32 s9, s9, 0
	global_load_dwordx4 v[172:175], v75, s[8:9]
	s_mov_b64 s[6:7], s[40:41]
	ds_read_b32 v226, v211
	ds_read_b32 v227, v211 offset:512
	ds_read_b32 v228, v211 offset:1024
	ds_read_b32 v229, v211 offset:1536
	ds_read_b32 v230, v211 offset:2048
	ds_read_b32 v231, v211 offset:2560
	ds_read_b32 v232, v211 offset:3072
	ds_read_b32 v233, v211 offset:3584
	ds_read_b32 v234, v211 offset:4096
	ds_read_b32 v235, v211 offset:4608
	ds_read_b32 v236, v211 offset:5120
	ds_read_b32 v237, v211 offset:5632
	ds_read_b32 v238, v211 offset:6144
	ds_read_b32 v239, v211 offset:6656
	ds_read_b32 v240, v211 offset:7168
	ds_read_b32 v241, v211 offset:7680
	s_waitcnt lgkmcnt(0)
	v_max_f32_e32 v226, v226, v226
	v_max_f32_e32 v227, v227, v227
	v_max_f32_e32 v228, v228, v228
	v_max_f32_e32 v229, v229, v229
	v_max_f32_e32 v230, v230, v230
	v_max_f32_e32 v231, v231, v231
	v_max_f32_e32 v232, v232, v232
	v_max_f32_e32 v233, v233, v233
	v_max_f32_e32 v234, v234, v234
	v_max_f32_e32 v235, v235, v235
	v_max_f32_e32 v236, v236, v236
	v_max_f32_e32 v237, v237, v237
	v_max_f32_e32 v238, v238, v238
	v_max_f32_e32 v239, v239, v239
	v_max_f32_e32 v240, v240, v240
	v_max_f32_e32 v241, v241, v241
	v_med3_f32 v226, v226, s62, v95
	v_med3_f32 v227, v227, s62, v95
	v_med3_f32 v228, v228, s62, v95
	v_med3_f32 v229, v229, s62, v95
	v_med3_f32 v230, v230, s62, v95
	v_med3_f32 v231, v231, s62, v95
	v_med3_f32 v232, v232, s62, v95
	v_med3_f32 v233, v233, s62, v95
	v_med3_f32 v234, v234, s62, v95
	v_med3_f32 v235, v235, s62, v95
	v_med3_f32 v236, v236, s62, v95
	v_med3_f32 v237, v237, s62, v95
	v_med3_f32 v238, v238, s62, v95
	v_med3_f32 v239, v239, s62, v95
	v_med3_f32 v240, v240, s62, v95
	v_med3_f32 v241, v241, s62, v95
	v_mov_b32_e32 v242, 0
	v_mov_b32_e32 v243, 0
	v_mov_b32_e32 v244, 0
	v_mov_b32_e32 v245, 0
	v_cvt_pk_fp8_f32 v242, v226, v227
	v_cvt_pk_fp8_f32 v243, v230, v231
	v_cvt_pk_fp8_f32 v244, v234, v235
	v_cvt_pk_fp8_f32 v245, v238, v239
	v_cvt_pk_fp8_f32 v242, v228, v229 op_sel:[0,0,1]
	v_cvt_pk_fp8_f32 v243, v232, v233 op_sel:[0,0,1]
	v_cvt_pk_fp8_f32 v244, v236, v237 op_sel:[0,0,1]
	v_cvt_pk_fp8_f32 v245, v240, v241 op_sel:[0,0,1]
	s_nop 0
	global_store_dwordx4 v79, v[242:245], s[6:7]
	ds_read_b32 v226, v213
	ds_read_b32 v227, v213 offset:512
	ds_read_b32 v228, v213 offset:1024
	ds_read_b32 v229, v213 offset:1536
	ds_read_b32 v230, v213 offset:2048
	ds_read_b32 v231, v213 offset:2560
	ds_read_b32 v232, v213 offset:3072
	ds_read_b32 v233, v213 offset:3584
	ds_read_b32 v234, v213 offset:4096
	ds_read_b32 v235, v213 offset:4608
	ds_read_b32 v236, v213 offset:5120
	ds_read_b32 v237, v213 offset:5632
	ds_read_b32 v238, v213 offset:6144
	ds_read_b32 v239, v213 offset:6656
	ds_read_b32 v240, v213 offset:7168
	ds_read_b32 v241, v213 offset:7680
	s_waitcnt lgkmcnt(0)
	v_max_f32_e32 v226, v226, v226
	v_max_f32_e32 v227, v227, v227
	v_max_f32_e32 v228, v228, v228
	v_max_f32_e32 v229, v229, v229
	v_max_f32_e32 v230, v230, v230
	v_max_f32_e32 v231, v231, v231
	v_max_f32_e32 v232, v232, v232
	v_max_f32_e32 v233, v233, v233
	v_max_f32_e32 v234, v234, v234
	v_max_f32_e32 v235, v235, v235
	v_max_f32_e32 v236, v236, v236
	v_max_f32_e32 v237, v237, v237
	v_max_f32_e32 v238, v238, v238
	v_max_f32_e32 v239, v239, v239
	v_max_f32_e32 v240, v240, v240
	v_max_f32_e32 v241, v241, v241
	v_med3_f32 v226, v226, s62, v95
	v_med3_f32 v227, v227, s62, v95
	v_med3_f32 v228, v228, s62, v95
	v_med3_f32 v229, v229, s62, v95
	v_med3_f32 v230, v230, s62, v95
	v_med3_f32 v231, v231, s62, v95
	v_med3_f32 v232, v232, s62, v95
	v_med3_f32 v233, v233, s62, v95
	v_med3_f32 v234, v234, s62, v95
	v_med3_f32 v235, v235, s62, v95
	v_med3_f32 v236, v236, s62, v95
	v_med3_f32 v237, v237, s62, v95
	v_med3_f32 v238, v238, s62, v95
	v_med3_f32 v239, v239, s62, v95
	v_med3_f32 v240, v240, s62, v95
	v_med3_f32 v241, v241, s62, v95
	v_mov_b32_e32 v242, 0
	v_mov_b32_e32 v243, 0
	v_mov_b32_e32 v244, 0
	v_mov_b32_e32 v245, 0
	v_cvt_pk_fp8_f32 v242, v226, v227
	v_cvt_pk_fp8_f32 v243, v230, v231
	v_cvt_pk_fp8_f32 v244, v234, v235
	v_cvt_pk_fp8_f32 v245, v238, v239
	v_cvt_pk_fp8_f32 v242, v228, v229 op_sel:[0,0,1]
	v_cvt_pk_fp8_f32 v243, v232, v233 op_sel:[0,0,1]
	v_cvt_pk_fp8_f32 v244, v236, v237 op_sel:[0,0,1]
	v_cvt_pk_fp8_f32 v245, v240, v241 op_sel:[0,0,1]
	s_nop 0
	global_store_dwordx4 v80, v[242:245], s[6:7]
	s_waitcnt vmcnt(12)
	v_mul_f32_e32 v176, 0x43000000, v176
	v_mul_f32_e32 v177, 0x43000000, v177
	v_mul_f32_e32 v178, 0x43000000, v178
	v_mul_f32_e32 v179, 0x43000000, v179
	ds_write_b128 v210, v[176:179]
	v_mul_f32_e32 v180, 0x43000000, v180
	v_mul_f32_e32 v181, 0x43000000, v181
	v_mul_f32_e32 v182, 0x43000000, v182
	v_mul_f32_e32 v183, 0x43000000, v183
	ds_write_b128 v210, v[180:183] offset:1024
	v_mul_f32_e32 v184, 0x43000000, v184
	v_mul_f32_e32 v185, 0x43000000, v185
	v_mul_f32_e32 v186, 0x43000000, v186
	v_mul_f32_e32 v187, 0x43000000, v187
	ds_write_b128 v210, v[184:187] offset:2048
	v_mul_f32_e32 v188, 0x43000000, v188
	v_mul_f32_e32 v189, 0x43000000, v189
	v_mul_f32_e32 v190, 0x43000000, v190
	v_mul_f32_e32 v191, 0x43000000, v191
	ds_write_b128 v210, v[188:191] offset:3072
	v_mul_f32_e32 v192, 0x43000000, v192
	v_mul_f32_e32 v193, 0x43000000, v193
	v_mul_f32_e32 v194, 0x43000000, v194
	v_mul_f32_e32 v195, 0x43000000, v195
	ds_write_b128 v210, v[192:195] offset:4096
	v_mul_f32_e32 v196, 0x43000000, v196
	v_mul_f32_e32 v197, 0x43000000, v197
	v_mul_f32_e32 v198, 0x43000000, v198
	v_mul_f32_e32 v199, 0x43000000, v199
	ds_write_b128 v210, v[196:199] offset:5120
	v_mul_f32_e32 v200, 0x43000000, v200
	v_mul_f32_e32 v201, 0x43000000, v201
	v_mul_f32_e32 v202, 0x43000000, v202
	v_mul_f32_e32 v203, 0x43000000, v203
	ds_write_b128 v210, v[200:203] offset:6144
	v_mul_f32_e32 v204, 0x43000000, v204
	v_mul_f32_e32 v205, 0x43000000, v205
	v_mul_f32_e32 v206, 0x43000000, v206
	v_mul_f32_e32 v207, 0x43000000, v207
	ds_write_b128 v210, v[204:207] offset:7168
	s_waitcnt lgkmcnt(0)
	s_barrier
; #define GAS __attribute__((address_space(1)))
; #define LAS __attribute__((address_space(3)))
; #define LDS_WAIT() asm volatile("s_waitcnt lgkmcnt(0)" ::: "memory")
; __device__ __forceinline__ unsigned pk4_fp8(float a, float b, float c, float d) {
;     a = fminf(fmaxf(a, -448.f), 448.f); b = fminf(fmaxf(b, -448.f), 448.f); c = fminf(fmaxf(c, -448.f), 448.f); d = fminf(fmaxf(d, -448.f), 448.f);
;     int w = __builtin_amdgcn_cvt_pk_fp8_f32(a, b, 0, false); w = __builtin_amdgcn_cvt_pk_fp8_f32(c, d, w, true); return (unsigned)w; }
;     ...
; #pragma unroll
;     for (int i = 0; i < 32; ++i) v[i] = sc >= 0 ? W[(size_t)(k0 + 2 * i + (lane >> 5)) * Nsrc + sc] : 0.f;
; #pragma unroll
;     for (int i = 0; i < 32; ++i) { const int k = k0 + 2 * i + (lane >> 5); float x = v[i] * wscale; if (KS) x *= (k < ksplit ? ksA[k] : ksB[k - ksplit]); scr[(2 * i + (lane >> 5)) * 33 + (lane & 31)] = x; }
;     LDS_WAIT(); asm volatile("" ::: "memory");
;     const int c = lane & 7;
; #pragma unroll
;     for (int j = 0; j < 4; ++j) { const int n = (lane >> 3) + 8 * j; const LAS float* s = scr + (8 * c) * 33 + n;
;         const unsigned long long o = (unsigned long long)pg8::pk4_fp8(s[0 * 33], s[1 * 33], s[2 * 33], s[3 * 33]) | ((unsigned long long)pg8::pk4_fp8(s[4 * 33], s[5 * 33], s[6 * 33], s[7 * 33]) << 32);
;         *(GAS unsigned long long*)(WT + (size_t)(n0 + n) * K + k0 + 8 * c) = o; }
;     LDS_WAIT(); asm volatile("" ::: "memory");
	s_add_u32 s8, s38, 0x3000
	s_addc_u32 s9, s39, 0
	global_load_dwordx4 v[176:179], v75, s[8:9]
	s_add_u32 s8, s8, 0x8000
	s_addc_u32 s9, s9, 0
	global_load_dwordx4 v[180:183], v75, s[8:9]
	s_add_u32 s8, s8, 0x8000
	s_addc_u32 s9, s9, 0
	global_load_dwordx4 v[184:187], v75, s[8:9]
	s_add_u32 s8, s8, 0x8000
	s_addc_u32 s9, s9, 0
	global_load_dwordx4 v[188:191], v75, s[8:9]
	s_add_u32 s8, s8, 0x8000
	s_addc_u32 s9, s9, 0
	global_load_dwordx4 v[192:195], v75, s[8:9]
	s_add_u32 s8, s8, 0x8000
	s_addc_u32 s9, s9, 0
	global_load_dwordx4 v[196:199], v75, s[8:9]
	s_add_u32 s8, s8, 0x8000
	s_addc_u32 s9, s9, 0
	global_load_dwordx4 v[200:203], v75, s[8:9]
	s_add_u32 s8, s8, 0x8000
	s_addc_u32 s9, s9, 0
	global_load_dwordx4 v[204:207], v75, s[8:9]
	s_add_u32 s6, s40, 0x1000000
	s_addc_u32 s7, s41, 0
	ds_read_b32 v226, v212
	ds_read_b32 v227, v212 offset:512
	ds_read_b32 v228, v212 offset:1024
	ds_read_b32 v229, v212 offset:1536
	ds_read_b32 v230, v212 offset:2048
	ds_read_b32 v231, v212 offset:2560
	ds_read_b32 v232, v212 offset:3072
	ds_read_b32 v233, v212 offset:3584
	ds_read_b32 v234, v212 offset:4096
	ds_read_b32 v235, v212 offset:4608
	ds_read_b32 v236, v212 offset:5120
	ds_read_b32 v237, v212 offset:5632
	ds_read_b32 v238, v212 offset:6144
	ds_read_b32 v239, v212 offset:6656
	ds_read_b32 v240, v212 offset:7168
	ds_read_b32 v241, v212 offset:7680
	s_waitcnt lgkmcnt(0)
	v_max_f32_e32 v226, v226, v226
	v_max_f32_e32 v227, v227, v227
	v_max_f32_e32 v228, v228, v228
	v_max_f32_e32 v229, v229, v229
	v_max_f32_e32 v230, v230, v230
	v_max_f32_e32 v231, v231, v231
	v_max_f32_e32 v232, v232, v232
	v_max_f32_e32 v233, v233, v233
	v_max_f32_e32 v234, v234, v234
	v_max_f32_e32 v235, v235, v235
	v_max_f32_e32 v236, v236, v236
	v_max_f32_e32 v237, v237, v237
	v_max_f32_e32 v238, v238, v238
	v_max_f32_e32 v239, v239, v239
	v_max_f32_e32 v240, v240, v240
	v_max_f32_e32 v241, v241, v241
	v_med3_f32 v226, v226, s62, v95
	v_med3_f32 v227, v227, s62, v95
	v_med3_f32 v228, v228, s62, v95
	v_med3_f32 v229, v229, s62, v95
	v_med3_f32 v230, v230, s62, v95
	v_med3_f32 v231, v231, s62, v95
	v_med3_f32 v232, v232, s62, v95
	v_med3_f32 v233, v233, s62, v95
	v_med3_f32 v234, v234, s62, v95
	v_med3_f32 v235, v235, s62, v95
	v_med3_f32 v236, v236, s62, v95
	v_med3_f32 v237, v237, s62, v95
	v_med3_f32 v238, v238, s62, v95
	v_med3_f32 v239, v239, s62, v95
	v_med3_f32 v240, v240, s62, v95
	v_med3_f32 v241, v241, s62, v95
	v_mov_b32_e32 v242, 0
	v_mov_b32_e32 v243, 0
	v_mov_b32_e32 v244, 0
	v_mov_b32_e32 v245, 0
	v_cvt_pk_fp8_f32 v242, v226, v227
	v_cvt_pk_fp8_f32 v243, v230, v231
	v_cvt_pk_fp8_f32 v244, v234, v235
	v_cvt_pk_fp8_f32 v245, v238, v239
	v_cvt_pk_fp8_f32 v242, v228, v229 op_sel:[0,0,1]
	v_cvt_pk_fp8_f32 v243, v232, v233 op_sel:[0,0,1]
	v_cvt_pk_fp8_f32 v244, v236, v237 op_sel:[0,0,1]
	v_cvt_pk_fp8_f32 v245, v240, v241 op_sel:[0,0,1]
	s_nop 0
	global_store_dwordx4 v79, v[242:245], s[6:7]
	ds_read_b32 v226, v214
	ds_read_b32 v227, v214 offset:512
	ds_read_b32 v228, v214 offset:1024
	ds_read_b32 v229, v214 offset:1536
	ds_read_b32 v230, v214 offset:2048
	ds_read_b32 v231, v214 offset:2560
	ds_read_b32 v232, v214 offset:3072
	ds_read_b32 v233, v214 offset:3584
	ds_read_b32 v234, v214 offset:4096
	ds_read_b32 v235, v214 offset:4608
	ds_read_b32 v236, v214 offset:5120
	ds_read_b32 v237, v214 offset:5632
	ds_read_b32 v238, v214 offset:6144
	ds_read_b32 v239, v214 offset:6656
	ds_read_b32 v240, v214 offset:7168
	ds_read_b32 v241, v214 offset:7680
	s_waitcnt lgkmcnt(0)
	v_max_f32_e32 v226, v226, v226
	v_max_f32_e32 v227, v227, v227
	v_max_f32_e32 v228, v228, v228
	v_max_f32_e32 v229, v229, v229
	v_max_f32_e32 v230, v230, v230
	v_max_f32_e32 v231, v231, v231
	v_max_f32_e32 v232, v232, v232
	v_max_f32_e32 v233, v233, v233
	v_max_f32_e32 v234, v234, v234
	v_max_f32_e32 v235, v235, v235
	v_max_f32_e32 v236, v236, v236
	v_max_f32_e32 v237, v237, v237
	v_max_f32_e32 v238, v238, v238
	v_max_f32_e32 v239, v239, v239
	v_max_f32_e32 v240, v240, v240
	v_max_f32_e32 v241, v241, v241
	v_med3_f32 v226, v226, s62, v95
	v_med3_f32 v227, v227, s62, v95
	v_med3_f32 v228, v228, s62, v95
	v_med3_f32 v229, v229, s62, v95
	v_med3_f32 v230, v230, s62, v95
	v_med3_f32 v231, v231, s62, v95
	v_med3_f32 v232, v232, s62, v95
	v_med3_f32 v233, v233, s62, v95
	v_med3_f32 v234, v234, s62, v95
	v_med3_f32 v235, v235, s62, v95
	v_med3_f32 v236, v236, s62, v95
	v_med3_f32 v237, v237, s62, v95
	v_med3_f32 v238, v238, s62, v95
	v_med3_f32 v239, v239, s62, v95
	v_med3_f32 v240, v240, s62, v95
	v_med3_f32 v241, v241, s62, v95
	v_mov_b32_e32 v242, 0
	v_mov_b32_e32 v243, 0
	v_mov_b32_e32 v244, 0
	v_mov_b32_e32 v245, 0
	v_cvt_pk_fp8_f32 v242, v226, v227
	v_cvt_pk_fp8_f32 v243, v230, v231
	v_cvt_pk_fp8_f32 v244, v234, v235
	v_cvt_pk_fp8_f32 v245, v238, v239
	v_cvt_pk_fp8_f32 v242, v228, v229 op_sel:[0,0,1]
	v_cvt_pk_fp8_f32 v243, v232, v233 op_sel:[0,0,1]
	v_cvt_pk_fp8_f32 v244, v236, v237 op_sel:[0,0,1]
	v_cvt_pk_fp8_f32 v245, v240, v241 op_sel:[0,0,1]
	s_nop 0
	global_store_dwordx4 v80, v[242:245], s[6:7]
	s_waitcnt vmcnt(12)
	v_mul_f32_e32 v144, 0x43000000, v144
	v_mul_f32_e32 v145, 0x43000000, v145
	v_mul_f32_e32 v146, 0x43000000, v146
	v_mul_f32_e32 v147, 0x43000000, v147
	ds_write_b128 v209, v[144:147]
	v_mul_f32_e32 v148, 0x43000000, v148
	v_mul_f32_e32 v149, 0x43000000, v149
	v_mul_f32_e32 v150, 0x43000000, v150
	v_mul_f32_e32 v151, 0x43000000, v151
	ds_write_b128 v209, v[148:151] offset:1024
	v_mul_f32_e32 v152, 0x43000000, v152
	v_mul_f32_e32 v153, 0x43000000, v153
	v_mul_f32_e32 v154, 0x43000000, v154
	v_mul_f32_e32 v155, 0x43000000, v155
	ds_write_b128 v209, v[152:155] offset:2048
	v_mul_f32_e32 v156, 0x43000000, v156
	v_mul_f32_e32 v157, 0x43000000, v157
	v_mul_f32_e32 v158, 0x43000000, v158
	v_mul_f32_e32 v159, 0x43000000, v159
	ds_write_b128 v209, v[156:159] offset:3072
	v_mul_f32_e32 v160, 0x43000000, v160
	v_mul_f32_e32 v161, 0x43000000, v161
	v_mul_f32_e32 v162, 0x43000000, v162
	v_mul_f32_e32 v163, 0x43000000, v163
	ds_write_b128 v209, v[160:163] offset:4096
	v_mul_f32_e32 v164, 0x43000000, v164
	v_mul_f32_e32 v165, 0x43000000, v165
	v_mul_f32_e32 v166, 0x43000000, v166
	v_mul_f32_e32 v167, 0x43000000, v167
	ds_write_b128 v209, v[164:167] offset:5120
	v_mul_f32_e32 v168, 0x43000000, v168
	v_mul_f32_e32 v169, 0x43000000, v169
	v_mul_f32_e32 v170, 0x43000000, v170
	v_mul_f32_e32 v171, 0x43000000, v171
	ds_write_b128 v209, v[168:171] offset:6144
	v_mul_f32_e32 v172, 0x43000000, v172
	v_mul_f32_e32 v173, 0x43000000, v173
	v_mul_f32_e32 v174, 0x43000000, v174
	v_mul_f32_e32 v175, 0x43000000, v175
	ds_write_b128 v209, v[172:175] offset:7168
	s_waitcnt lgkmcnt(0)
	s_barrier
; #define GAS __attribute__((address_space(1)))
; #define LAS __attribute__((address_space(3)))
; #define LDS_WAIT() asm volatile("s_waitcnt lgkmcnt(0)" ::: "memory")
; __device__ __forceinline__ unsigned pk4_fp8(float a, float b, float c, float d) {
;     a = fminf(fmaxf(a, -448.f), 448.f); b = fminf(fmaxf(b, -448.f), 448.f); c = fminf(fmaxf(c, -448.f), 448.f); d = fminf(fmaxf(d, -448.f), 448.f);
;     int w = __builtin_amdgcn_cvt_pk_fp8_f32(a, b, 0, false); w = __builtin_amdgcn_cvt_pk_fp8_f32(c, d, w, true); return (unsigned)w; }
;     ...
; #pragma unroll
;     for (int i = 0; i < 32; ++i) v[i] = sc >= 0 ? W[(size_t)(k0 + 2 * i + (lane >> 5)) * Nsrc + sc] : 0.f;
; #pragma unroll
;     for (int i = 0; i < 32; ++i) { const int k = k0 + 2 * i + (lane >> 5); float x = v[i] * wscale; if (KS) x *= (k < ksplit ? ksA[k] : ksB[k - ksplit]); scr[(2 * i + (lane >> 5)) * 33 + (lane & 31)] = x; }
;     LDS_WAIT(); asm volatile("" ::: "memory");
;     const int c = lane & 7;
; #pragma unroll
;     for (int j = 0; j < 4; ++j) { const int n = (lane >> 3) + 8 * j; const LAS float* s = scr + (8 * c) * 33 + n;
;         const unsigned long long o = (unsigned long long)pg8::pk4_fp8(s[0 * 33], s[1 * 33], s[2 * 33], s[3 * 33]) | ((unsigned long long)pg8::pk4_fp8(s[4 * 33], s[5 * 33], s[6 * 33], s[7 * 33]) << 32);
;         *(GAS unsigned long long*)(WT + (size_t)(n0 + n) * K + k0 + 8 * c) = o; }
;     LDS_WAIT(); asm volatile("" ::: "memory");
	s_add_u32 s8, s38, 0x4000000
	s_addc_u32 s9, s39, 0
	global_load_dwordx4 v[144:147], v75, s[8:9]
	s_add_u32 s8, s8, 0x8000
	s_addc_u32 s9, s9, 0
	global_load_dwordx4 v[148:151], v75, s[8:9]
	s_add_u32 s8, s8, 0x8000
	s_addc_u32 s9, s9, 0
	global_load_dwordx4 v[152:155], v75, s[8:9]
	s_add_u32 s8, s8, 0x8000
	s_addc_u32 s9, s9, 0
	global_load_dwordx4 v[156:159], v75, s[8:9]
	s_add_u32 s8, s8, 0x8000
	s_addc_u32 s9, s9, 0
	global_load_dwordx4 v[160:163], v75, s[8:9]
	s_add_u32 s8, s8, 0x8000
	s_addc_u32 s9, s9, 0
	global_load_dwordx4 v[164:167], v75, s[8:9]
	s_add_u32 s8, s8, 0x8000
	s_addc_u32 s9, s9, 0
	global_load_dwordx4 v[168:171], v75, s[8:9]
	s_add_u32 s8, s8, 0x8000
	s_addc_u32 s9, s9, 0
	global_load_dwordx4 v[172:175], v75, s[8:9]
	s_add_u32 s6, s40, 0x2000000
	s_addc_u32 s7, s41, 0
	ds_read_b32 v226, v211
	ds_read_b32 v227, v211 offset:512
	ds_read_b32 v228, v211 offset:1024
	ds_read_b32 v229, v211 offset:1536
	ds_read_b32 v230, v211 offset:2048
	ds_read_b32 v231, v211 offset:2560
	ds_read_b32 v232, v211 offset:3072
	ds_read_b32 v233, v211 offset:3584
	ds_read_b32 v234, v211 offset:4096
	ds_read_b32 v235, v211 offset:4608
	ds_read_b32 v236, v211 offset:5120
	ds_read_b32 v237, v211 offset:5632
	ds_read_b32 v238, v211 offset:6144
	ds_read_b32 v239, v211 offset:6656
	ds_read_b32 v240, v211 offset:7168
	ds_read_b32 v241, v211 offset:7680
	s_waitcnt lgkmcnt(0)
	v_max_f32_e32 v226, v226, v226
	v_max_f32_e32 v227, v227, v227
	v_max_f32_e32 v228, v228, v228
	v_max_f32_e32 v229, v229, v229
	v_max_f32_e32 v230, v230, v230
	v_max_f32_e32 v231, v231, v231
	v_max_f32_e32 v232, v232, v232
	v_max_f32_e32 v233, v233, v233
	v_max_f32_e32 v234, v234, v234
	v_max_f32_e32 v235, v235, v235
	v_max_f32_e32 v236, v236, v236
	v_max_f32_e32 v237, v237, v237
	v_max_f32_e32 v238, v238, v238
	v_max_f32_e32 v239, v239, v239
	v_max_f32_e32 v240, v240, v240
	v_max_f32_e32 v241, v241, v241
	v_med3_f32 v226, v226, s62, v95
	v_med3_f32 v227, v227, s62, v95
	v_med3_f32 v228, v228, s62, v95
	v_med3_f32 v229, v229, s62, v95
	v_med3_f32 v230, v230, s62, v95
	v_med3_f32 v231, v231, s62, v95
	v_med3_f32 v232, v232, s62, v95
	v_med3_f32 v233, v233, s62, v95
	v_med3_f32 v234, v234, s62, v95
	v_med3_f32 v235, v235, s62, v95
	v_med3_f32 v236, v236, s62, v95
	v_med3_f32 v237, v237, s62, v95
	v_med3_f32 v238, v238, s62, v95
	v_med3_f32 v239, v239, s62, v95
	v_med3_f32 v240, v240, s62, v95
	v_med3_f32 v241, v241, s62, v95
	v_mov_b32_e32 v242, 0
	v_mov_b32_e32 v243, 0
	v_mov_b32_e32 v244, 0
	v_mov_b32_e32 v245, 0
	v_cvt_pk_fp8_f32 v242, v226, v227
	v_cvt_pk_fp8_f32 v243, v230, v231
	v_cvt_pk_fp8_f32 v244, v234, v235
	v_cvt_pk_fp8_f32 v245, v238, v239
	v_cvt_pk_fp8_f32 v242, v228, v229 op_sel:[0,0,1]
	v_cvt_pk_fp8_f32 v243, v232, v233 op_sel:[0,0,1]
	v_cvt_pk_fp8_f32 v244, v236, v237 op_sel:[0,0,1]
	v_cvt_pk_fp8_f32 v245, v240, v241 op_sel:[0,0,1]
	s_nop 0
	global_store_dwordx4 v79, v[242:245], s[6:7]
	ds_read_b32 v226, v213
	ds_read_b32 v227, v213 offset:512
	ds_read_b32 v228, v213 offset:1024
	ds_read_b32 v229, v213 offset:1536
	ds_read_b32 v230, v213 offset:2048
	ds_read_b32 v231, v213 offset:2560
	ds_read_b32 v232, v213 offset:3072
	ds_read_b32 v233, v213 offset:3584
	ds_read_b32 v234, v213 offset:4096
	ds_read_b32 v235, v213 offset:4608
	ds_read_b32 v236, v213 offset:5120
	ds_read_b32 v237, v213 offset:5632
	ds_read_b32 v238, v213 offset:6144
	ds_read_b32 v239, v213 offset:6656
	ds_read_b32 v240, v213 offset:7168
	ds_read_b32 v241, v213 offset:7680
	s_waitcnt lgkmcnt(0)
	v_max_f32_e32 v226, v226, v226
	v_max_f32_e32 v227, v227, v227
	v_max_f32_e32 v228, v228, v228
	v_max_f32_e32 v229, v229, v229
	v_max_f32_e32 v230, v230, v230
	v_max_f32_e32 v231, v231, v231
	v_max_f32_e32 v232, v232, v232
	v_max_f32_e32 v233, v233, v233
	v_max_f32_e32 v234, v234, v234
	v_max_f32_e32 v235, v235, v235
	v_max_f32_e32 v236, v236, v236
	v_max_f32_e32 v237, v237, v237
	v_max_f32_e32 v238, v238, v238
	v_max_f32_e32 v239, v239, v239
	v_max_f32_e32 v240, v240, v240
	v_max_f32_e32 v241, v241, v241
	v_med3_f32 v226, v226, s62, v95
	v_med3_f32 v227, v227, s62, v95
	v_med3_f32 v228, v228, s62, v95
	v_med3_f32 v229, v229, s62, v95
	v_med3_f32 v230, v230, s62, v95
	v_med3_f32 v231, v231, s62, v95
	v_med3_f32 v232, v232, s62, v95
	v_med3_f32 v233, v233, s62, v95
	v_med3_f32 v234, v234, s62, v95
	v_med3_f32 v235, v235, s62, v95
	v_med3_f32 v236, v236, s62, v95
	v_med3_f32 v237, v237, s62, v95
	v_med3_f32 v238, v238, s62, v95
	v_med3_f32 v239, v239, s62, v95
	v_med3_f32 v240, v240, s62, v95
	v_med3_f32 v241, v241, s62, v95
	v_mov_b32_e32 v242, 0
	v_mov_b32_e32 v243, 0
	v_mov_b32_e32 v244, 0
	v_mov_b32_e32 v245, 0
	v_cvt_pk_fp8_f32 v242, v226, v227
	v_cvt_pk_fp8_f32 v243, v230, v231
	v_cvt_pk_fp8_f32 v244, v234, v235
	v_cvt_pk_fp8_f32 v245, v238, v239
	v_cvt_pk_fp8_f32 v242, v228, v229 op_sel:[0,0,1]
	v_cvt_pk_fp8_f32 v243, v232, v233 op_sel:[0,0,1]
	v_cvt_pk_fp8_f32 v244, v236, v237 op_sel:[0,0,1]
	v_cvt_pk_fp8_f32 v245, v240, v241 op_sel:[0,0,1]
	s_nop 0
	global_store_dwordx4 v80, v[242:245], s[6:7]
	s_waitcnt vmcnt(12)
	v_mul_f32_e32 v176, 0x43000000, v176
	v_mul_f32_e32 v177, 0x43000000, v177
	v_mul_f32_e32 v178, 0x43000000, v178
	v_mul_f32_e32 v179, 0x43000000, v179
	ds_write_b128 v210, v[176:179]
	v_mul_f32_e32 v180, 0x43000000, v180
	v_mul_f32_e32 v181, 0x43000000, v181
	v_mul_f32_e32 v182, 0x43000000, v182
	v_mul_f32_e32 v183, 0x43000000, v183
	ds_write_b128 v210, v[180:183] offset:1024
	v_mul_f32_e32 v184, 0x43000000, v184
	v_mul_f32_e32 v185, 0x43000000, v185
	v_mul_f32_e32 v186, 0x43000000, v186
	v_mul_f32_e32 v187, 0x43000000, v187
	ds_write_b128 v210, v[184:187] offset:2048
	v_mul_f32_e32 v188, 0x43000000, v188
	v_mul_f32_e32 v189, 0x43000000, v189
	v_mul_f32_e32 v190, 0x43000000, v190
	v_mul_f32_e32 v191, 0x43000000, v191
	ds_write_b128 v210, v[188:191] offset:3072
	v_mul_f32_e32 v192, 0x43000000, v192
	v_mul_f32_e32 v193, 0x43000000, v193
	v_mul_f32_e32 v194, 0x43000000, v194
	v_mul_f32_e32 v195, 0x43000000, v195
	ds_write_b128 v210, v[192:195] offset:4096
	v_mul_f32_e32 v196, 0x43000000, v196
	v_mul_f32_e32 v197, 0x43000000, v197
	v_mul_f32_e32 v198, 0x43000000, v198
	v_mul_f32_e32 v199, 0x43000000, v199
	ds_write_b128 v210, v[196:199] offset:5120
	v_mul_f32_e32 v200, 0x43000000, v200
	v_mul_f32_e32 v201, 0x43000000, v201
	v_mul_f32_e32 v202, 0x43000000, v202
	v_mul_f32_e32 v203, 0x43000000, v203
	ds_write_b128 v210, v[200:203] offset:6144
	v_mul_f32_e32 v204, 0x43000000, v204
	v_mul_f32_e32 v205, 0x43000000, v205
	v_mul_f32_e32 v206, 0x43000000, v206
	v_mul_f32_e32 v207, 0x43000000, v207
	ds_write_b128 v210, v[204:207] offset:7168
	s_waitcnt lgkmcnt(0)
	s_barrier
; #define GAS __attribute__((address_space(1)))
; #define LAS __attribute__((address_space(3)))
; #define LDS_WAIT() asm volatile("s_waitcnt lgkmcnt(0)" ::: "memory")
; __device__ __forceinline__ unsigned pk4_fp8(float a, float b, float c, float d) {
;     a = fminf(fmaxf(a, -448.f), 448.f); b = fminf(fmaxf(b, -448.f), 448.f); c = fminf(fmaxf(c, -448.f), 448.f); d = fminf(fmaxf(d, -448.f), 448.f);
;     int w = __builtin_amdgcn_cvt_pk_fp8_f32(a, b, 0, false); w = __builtin_amdgcn_cvt_pk_fp8_f32(c, d, w, true); return (unsigned)w; }
;     ...
; #pragma unroll
;     for (int i = 0; i < 32; ++i) v[i] = sc >= 0 ? W[(size_t)(k0 + 2 * i + (lane >> 5)) * Nsrc + sc] : 0.f;
; #pragma unroll
;     for (int i = 0; i < 32; ++i) { const int k = k0 + 2 * i + (lane >> 5); float x = v[i] * wscale; if (KS) x *= (k < ksplit ? ksA[k] : ksB[k - ksplit]); scr[(2 * i + (lane >> 5)) * 33 + (lane & 31)] = x; }
;     LDS_WAIT(); asm volatile("" ::: "memory");
;     const int c = lane & 7;
; #pragma unroll
;     for (int j = 0; j < 4; ++j) { const int n = (lane >> 3) + 8 * j; const LAS float* s = scr + (8 * c) * 33 + n;
;         const unsigned long long o = (unsigned long long)pg8::pk4_fp8(s[0 * 33], s[1 * 33], s[2 * 33], s[3 * 33]) | ((unsigned long long)pg8::pk4_fp8(s[4 * 33], s[5 * 33], s[6 * 33], s[7 * 33]) << 32);
;         *(GAS unsigned long long*)(WT + (size_t)(n0 + n) * K + k0 + 8 * c) = o; }
;     LDS_WAIT(); asm volatile("" ::: "memory");
	s_add_u32 s8, s38, 0x4001000
	s_addc_u32 s9, s39, 0
	global_load_dwordx4 v[176:179], v75, s[8:9]
	s_add_u32 s8, s8, 0x8000
	s_addc_u32 s9, s9, 0
	global_load_dwordx4 v[180:183], v75, s[8:9]
	s_add_u32 s8, s8, 0x8000
	s_addc_u32 s9, s9, 0
	global_load_dwordx4 v[184:187], v75, s[8:9]
	s_add_u32 s8, s8, 0x8000
	s_addc_u32 s9, s9, 0
	global_load_dwordx4 v[188:191], v75, s[8:9]
	s_add_u32 s8, s8, 0x8000
	s_addc_u32 s9, s9, 0
	global_load_dwordx4 v[192:195], v75, s[8:9]
	s_add_u32 s8, s8, 0x8000
	s_addc_u32 s9, s9, 0
	global_load_dwordx4 v[196:199], v75, s[8:9]
	s_add_u32 s8, s8, 0x8000
	s_addc_u32 s9, s9, 0
	global_load_dwordx4 v[200:203], v75, s[8:9]
	s_add_u32 s8, s8, 0x8000
	s_addc_u32 s9, s9, 0
	global_load_dwordx4 v[204:207], v75, s[8:9]
	s_add_u32 s6, s40, 0x3000000
	s_addc_u32 s7, s41, 0
	ds_read_b32 v226, v212
	ds_read_b32 v227, v212 offset:512
	ds_read_b32 v228, v212 offset:1024
	ds_read_b32 v229, v212 offset:1536
	ds_read_b32 v230, v212 offset:2048
	ds_read_b32 v231, v212 offset:2560
	ds_read_b32 v232, v212 offset:3072
	ds_read_b32 v233, v212 offset:3584
	ds_read_b32 v234, v212 offset:4096
	ds_read_b32 v235, v212 offset:4608
	ds_read_b32 v236, v212 offset:5120
	ds_read_b32 v237, v212 offset:5632
	ds_read_b32 v238, v212 offset:6144
	ds_read_b32 v239, v212 offset:6656
	ds_read_b32 v240, v212 offset:7168
	ds_read_b32 v241, v212 offset:7680
	s_waitcnt lgkmcnt(0)
	v_max_f32_e32 v226, v226, v226
	v_max_f32_e32 v227, v227, v227
	v_max_f32_e32 v228, v228, v228
	v_max_f32_e32 v229, v229, v229
	v_max_f32_e32 v230, v230, v230
	v_max_f32_e32 v231, v231, v231
	v_max_f32_e32 v232, v232, v232
	v_max_f32_e32 v233, v233, v233
	v_max_f32_e32 v234, v234, v234
	v_max_f32_e32 v235, v235, v235
	v_max_f32_e32 v236, v236, v236
	v_max_f32_e32 v237, v237, v237
	v_max_f32_e32 v238, v238, v238
	v_max_f32_e32 v239, v239, v239
	v_max_f32_e32 v240, v240, v240
	v_max_f32_e32 v241, v241, v241
	v_med3_f32 v226, v226, s62, v95
	v_med3_f32 v227, v227, s62, v95
	v_med3_f32 v228, v228, s62, v95
	v_med3_f32 v229, v229, s62, v95
	v_med3_f32 v230, v230, s62, v95
	v_med3_f32 v231, v231, s62, v95
	v_med3_f32 v232, v232, s62, v95
	v_med3_f32 v233, v233, s62, v95
	v_med3_f32 v234, v234, s62, v95
	v_med3_f32 v235, v235, s62, v95
	v_med3_f32 v236, v236, s62, v95
	v_med3_f32 v237, v237, s62, v95
	v_med3_f32 v238, v238, s62, v95
	v_med3_f32 v239, v239, s62, v95
	v_med3_f32 v240, v240, s62, v95
	v_med3_f32 v241, v241, s62, v95
	v_mov_b32_e32 v242, 0
	v_mov_b32_e32 v243, 0
	v_mov_b32_e32 v244, 0
	v_mov_b32_e32 v245, 0
	v_cvt_pk_fp8_f32 v242, v226, v227
	v_cvt_pk_fp8_f32 v243, v230, v231
	v_cvt_pk_fp8_f32 v244, v234, v235
	v_cvt_pk_fp8_f32 v245, v238, v239
	v_cvt_pk_fp8_f32 v242, v228, v229 op_sel:[0,0,1]
	v_cvt_pk_fp8_f32 v243, v232, v233 op_sel:[0,0,1]
	v_cvt_pk_fp8_f32 v244, v236, v237 op_sel:[0,0,1]
	v_cvt_pk_fp8_f32 v245, v240, v241 op_sel:[0,0,1]
	s_nop 0
	global_store_dwordx4 v79, v[242:245], s[6:7]
	ds_read_b32 v226, v214
	ds_read_b32 v227, v214 offset:512
	ds_read_b32 v228, v214 offset:1024
	ds_read_b32 v229, v214 offset:1536
	ds_read_b32 v230, v214 offset:2048
	ds_read_b32 v231, v214 offset:2560
	ds_read_b32 v232, v214 offset:3072
	ds_read_b32 v233, v214 offset:3584
	ds_read_b32 v234, v214 offset:4096
	ds_read_b32 v235, v214 offset:4608
	ds_read_b32 v236, v214 offset:5120
	ds_read_b32 v237, v214 offset:5632
	ds_read_b32 v238, v214 offset:6144
	ds_read_b32 v239, v214 offset:6656
	ds_read_b32 v240, v214 offset:7168
	ds_read_b32 v241, v214 offset:7680
	s_waitcnt lgkmcnt(0)
	v_max_f32_e32 v226, v226, v226
	v_max_f32_e32 v227, v227, v227
	v_max_f32_e32 v228, v228, v228
	v_max_f32_e32 v229, v229, v229
	v_max_f32_e32 v230, v230, v230
	v_max_f32_e32 v231, v231, v231
	v_max_f32_e32 v232, v232, v232
	v_max_f32_e32 v233, v233, v233
	v_max_f32_e32 v234, v234, v234
	v_max_f32_e32 v235, v235, v235
	v_max_f32_e32 v236, v236, v236
	v_max_f32_e32 v237, v237, v237
	v_max_f32_e32 v238, v238, v238
	v_max_f32_e32 v239, v239, v239
	v_max_f32_e32 v240, v240, v240
	v_max_f32_e32 v241, v241, v241
	v_med3_f32 v226, v226, s62, v95
	v_med3_f32 v227, v227, s62, v95
	v_med3_f32 v228, v228, s62, v95
	v_med3_f32 v229, v229, s62, v95
	v_med3_f32 v230, v230, s62, v95
	v_med3_f32 v231, v231, s62, v95
	v_med3_f32 v232, v232, s62, v95
	v_med3_f32 v233, v233, s62, v95
	v_med3_f32 v234, v234, s62, v95
	v_med3_f32 v235, v235, s62, v95
	v_med3_f32 v236, v236, s62, v95
	v_med3_f32 v237, v237, s62, v95
	v_med3_f32 v238, v238, s62, v95
	v_med3_f32 v239, v239, s62, v95
	v_med3_f32 v240, v240, s62, v95
	v_med3_f32 v241, v241, s62, v95
	v_mov_b32_e32 v242, 0
	v_mov_b32_e32 v243, 0
	v_mov_b32_e32 v244, 0
	v_mov_b32_e32 v245, 0
	v_cvt_pk_fp8_f32 v242, v226, v227
	v_cvt_pk_fp8_f32 v243, v230, v231
	v_cvt_pk_fp8_f32 v244, v234, v235
	v_cvt_pk_fp8_f32 v245, v238, v239
	v_cvt_pk_fp8_f32 v242, v228, v229 op_sel:[0,0,1]
	v_cvt_pk_fp8_f32 v243, v232, v233 op_sel:[0,0,1]
	v_cvt_pk_fp8_f32 v244, v236, v237 op_sel:[0,0,1]
	v_cvt_pk_fp8_f32 v245, v240, v241 op_sel:[0,0,1]
	s_nop 0
	global_store_dwordx4 v80, v[242:245], s[6:7]
	s_waitcnt vmcnt(12)
	v_mul_f32_e32 v144, 0x43000000, v144
	v_mul_f32_e32 v145, 0x43000000, v145
	v_mul_f32_e32 v146, 0x43000000, v146
	v_mul_f32_e32 v147, 0x43000000, v147
	ds_write_b128 v209, v[144:147]
	v_mul_f32_e32 v148, 0x43000000, v148
	v_mul_f32_e32 v149, 0x43000000, v149
	v_mul_f32_e32 v150, 0x43000000, v150
	v_mul_f32_e32 v151, 0x43000000, v151
	ds_write_b128 v209, v[148:151] offset:1024
	v_mul_f32_e32 v152, 0x43000000, v152
	v_mul_f32_e32 v153, 0x43000000, v153
	v_mul_f32_e32 v154, 0x43000000, v154
	v_mul_f32_e32 v155, 0x43000000, v155
	ds_write_b128 v209, v[152:155] offset:2048
	v_mul_f32_e32 v156, 0x43000000, v156
	v_mul_f32_e32 v157, 0x43000000, v157
	v_mul_f32_e32 v158, 0x43000000, v158
	v_mul_f32_e32 v159, 0x43000000, v159
	ds_write_b128 v209, v[156:159] offset:3072
	v_mul_f32_e32 v160, 0x43000000, v160
	v_mul_f32_e32 v161, 0x43000000, v161
	v_mul_f32_e32 v162, 0x43000000, v162
	v_mul_f32_e32 v163, 0x43000000, v163
	ds_write_b128 v209, v[160:163] offset:4096
	v_mul_f32_e32 v164, 0x43000000, v164
	v_mul_f32_e32 v165, 0x43000000, v165
	v_mul_f32_e32 v166, 0x43000000, v166
	v_mul_f32_e32 v167, 0x43000000, v167
	ds_write_b128 v209, v[164:167] offset:5120
	v_mul_f32_e32 v168, 0x43000000, v168
	v_mul_f32_e32 v169, 0x43000000, v169
	v_mul_f32_e32 v170, 0x43000000, v170
	v_mul_f32_e32 v171, 0x43000000, v171
	ds_write_b128 v209, v[168:171] offset:6144
	v_mul_f32_e32 v172, 0x43000000, v172
	v_mul_f32_e32 v173, 0x43000000, v173
	v_mul_f32_e32 v174, 0x43000000, v174
	v_mul_f32_e32 v175, 0x43000000, v175
	ds_write_b128 v209, v[172:175] offset:7168
	s_waitcnt lgkmcnt(0)
	s_barrier
; #define GAS __attribute__((address_space(1)))
; #define LAS __attribute__((address_space(3)))
; #define LDS_WAIT() asm volatile("s_waitcnt lgkmcnt(0)" ::: "memory")
; __device__ __forceinline__ unsigned pk4_fp8(float a, float b, float c, float d) {
;     a = fminf(fmaxf(a, -448.f), 448.f); b = fminf(fmaxf(b, -448.f), 448.f); c = fminf(fmaxf(c, -448.f), 448.f); d = fminf(fmaxf(d, -448.f), 448.f);
;     int w = __builtin_amdgcn_cvt_pk_fp8_f32(a, b, 0, false); w = __builtin_amdgcn_cvt_pk_fp8_f32(c, d, w, true); return (unsigned)w; }
;     ...
; #pragma unroll
;     for (int i = 0; i < 32; ++i) v[i] = sc >= 0 ? W[(size_t)(k0 + 2 * i + (lane >> 5)) * Nsrc + sc] : 0.f;
; #pragma unroll
;     for (int i = 0; i < 32; ++i) { const int k = k0 + 2 * i + (lane >> 5); float x = v[i] * wscale; if (KS) x *= (k < ksplit ? ksA[k] : ksB[k - ksplit]); scr[(2 * i + (lane >> 5)) * 33 + (lane & 31)] = x; }
;     LDS_WAIT(); asm volatile("" ::: "memory");
;     const int c = lane & 7;
; #pragma unroll
;     for (int j = 0; j < 4; ++j) { const int n = (lane >> 3) + 8 * j; const LAS float* s = scr + (8 * c) * 33 + n;
;         const unsigned long long o = (unsigned long long)pg8::pk4_fp8(s[0 * 33], s[1 * 33], s[2 * 33], s[3 * 33]) | ((unsigned long long)pg8::pk4_fp8(s[4 * 33], s[5 * 33], s[6 * 33], s[7 * 33]) << 32);
;         *(GAS unsigned long long*)(WT + (size_t)(n0 + n) * K + k0 + 8 * c) = o; }
;     LDS_WAIT(); asm volatile("" ::: "memory");
	s_add_u32 s8, s38, 0x4002000
	s_addc_u32 s9, s39, 0
	global_load_dwordx4 v[144:147], v75, s[8:9]
	s_add_u32 s8, s8, 0x8000
	s_addc_u32 s9, s9, 0
	global_load_dwordx4 v[148:151], v75, s[8:9]
	s_add_u32 s8, s8, 0x8000
	s_addc_u32 s9, s9, 0
	global_load_dwordx4 v[152:155], v75, s[8:9]
	s_add_u32 s8, s8, 0x8000
	s_addc_u32 s9, s9, 0
	global_load_dwordx4 v[156:159], v75, s[8:9]
	s_add_u32 s8, s8, 0x8000
	s_addc_u32 s9, s9, 0
	global_load_dwordx4 v[160:163], v75, s[8:9]
	s_add_u32 s8, s8, 0x8000
	s_addc_u32 s9, s9, 0
	global_load_dwordx4 v[164:167], v75, s[8:9]
	s_add_u32 s8, s8, 0x8000
	s_addc_u32 s9, s9, 0
	global_load_dwordx4 v[168:171], v75, s[8:9]
	s_add_u32 s8, s8, 0x8000
	s_addc_u32 s9, s9, 0
	global_load_dwordx4 v[172:175], v75, s[8:9]
	s_add_u32 s6, s40, 0x1000
	s_addc_u32 s7, s41, 0
	ds_read_b32 v226, v211
	ds_read_b32 v227, v211 offset:512
	ds_read_b32 v228, v211 offset:1024
	ds_read_b32 v229, v211 offset:1536
	ds_read_b32 v230, v211 offset:2048
	ds_read_b32 v231, v211 offset:2560
	ds_read_b32 v232, v211 offset:3072
	ds_read_b32 v233, v211 offset:3584
	ds_read_b32 v234, v211 offset:4096
	ds_read_b32 v235, v211 offset:4608
	ds_read_b32 v236, v211 offset:5120
	ds_read_b32 v237, v211 offset:5632
	ds_read_b32 v238, v211 offset:6144
	ds_read_b32 v239, v211 offset:6656
	ds_read_b32 v240, v211 offset:7168
	ds_read_b32 v241, v211 offset:7680
	s_waitcnt lgkmcnt(0)
	v_max_f32_e32 v226, v226, v226
	v_max_f32_e32 v227, v227, v227
	v_max_f32_e32 v228, v228, v228
	v_max_f32_e32 v229, v229, v229
	v_max_f32_e32 v230, v230, v230
	v_max_f32_e32 v231, v231, v231
	v_max_f32_e32 v232, v232, v232
	v_max_f32_e32 v233, v233, v233
	v_max_f32_e32 v234, v234, v234
	v_max_f32_e32 v235, v235, v235
	v_max_f32_e32 v236, v236, v236
	v_max_f32_e32 v237, v237, v237
	v_max_f32_e32 v238, v238, v238
	v_max_f32_e32 v239, v239, v239
	v_max_f32_e32 v240, v240, v240
	v_max_f32_e32 v241, v241, v241
	v_med3_f32 v226, v226, s62, v95
	v_med3_f32 v227, v227, s62, v95
	v_med3_f32 v228, v228, s62, v95
	v_med3_f32 v229, v229, s62, v95
	v_med3_f32 v230, v230, s62, v95
	v_med3_f32 v231, v231, s62, v95
	v_med3_f32 v232, v232, s62, v95
	v_med3_f32 v233, v233, s62, v95
	v_med3_f32 v234, v234, s62, v95
	v_med3_f32 v235, v235, s62, v95
	v_med3_f32 v236, v236, s62, v95
	v_med3_f32 v237, v237, s62, v95
	v_med3_f32 v238, v238, s62, v95
	v_med3_f32 v239, v239, s62, v95
	v_med3_f32 v240, v240, s62, v95
	v_med3_f32 v241, v241, s62, v95
	v_mov_b32_e32 v242, 0
	v_mov_b32_e32 v243, 0
	v_mov_b32_e32 v244, 0
	v_mov_b32_e32 v245, 0
	v_cvt_pk_fp8_f32 v242, v226, v227
	v_cvt_pk_fp8_f32 v243, v230, v231
	v_cvt_pk_fp8_f32 v244, v234, v235
	v_cvt_pk_fp8_f32 v245, v238, v239
	v_cvt_pk_fp8_f32 v242, v228, v229 op_sel:[0,0,1]
	v_cvt_pk_fp8_f32 v243, v232, v233 op_sel:[0,0,1]
	v_cvt_pk_fp8_f32 v244, v236, v237 op_sel:[0,0,1]
	v_cvt_pk_fp8_f32 v245, v240, v241 op_sel:[0,0,1]
	s_nop 0
	global_store_dwordx4 v79, v[242:245], s[6:7]
	ds_read_b32 v226, v213
	ds_read_b32 v227, v213 offset:512
	ds_read_b32 v228, v213 offset:1024
	ds_read_b32 v229, v213 offset:1536
	ds_read_b32 v230, v213 offset:2048
	ds_read_b32 v231, v213 offset:2560
	ds_read_b32 v232, v213 offset:3072
	ds_read_b32 v233, v213 offset:3584
	ds_read_b32 v234, v213 offset:4096
	ds_read_b32 v235, v213 offset:4608
	ds_read_b32 v236, v213 offset:5120
	ds_read_b32 v237, v213 offset:5632
	ds_read_b32 v238, v213 offset:6144
	ds_read_b32 v239, v213 offset:6656
	ds_read_b32 v240, v213 offset:7168
	ds_read_b32 v241, v213 offset:7680
	s_waitcnt lgkmcnt(0)
	v_max_f32_e32 v226, v226, v226
	v_max_f32_e32 v227, v227, v227
	v_max_f32_e32 v228, v228, v228
	v_max_f32_e32 v229, v229, v229
	v_max_f32_e32 v230, v230, v230
	v_max_f32_e32 v231, v231, v231
	v_max_f32_e32 v232, v232, v232
	v_max_f32_e32 v233, v233, v233
	v_max_f32_e32 v234, v234, v234
	v_max_f32_e32 v235, v235, v235
	v_max_f32_e32 v236, v236, v236
	v_max_f32_e32 v237, v237, v237
	v_max_f32_e32 v238, v238, v238
	v_max_f32_e32 v239, v239, v239
	v_max_f32_e32 v240, v240, v240
	v_max_f32_e32 v241, v241, v241
	v_med3_f32 v226, v226, s62, v95
	v_med3_f32 v227, v227, s62, v95
	v_med3_f32 v228, v228, s62, v95
	v_med3_f32 v229, v229, s62, v95
	v_med3_f32 v230, v230, s62, v95
	v_med3_f32 v231, v231, s62, v95
	v_med3_f32 v232, v232, s62, v95
	v_med3_f32 v233, v233, s62, v95
	v_med3_f32 v234, v234, s62, v95
	v_med3_f32 v235, v235, s62, v95
	v_med3_f32 v236, v236, s62, v95
	v_med3_f32 v237, v237, s62, v95
	v_med3_f32 v238, v238, s62, v95
	v_med3_f32 v239, v239, s62, v95
	v_med3_f32 v240, v240, s62, v95
	v_med3_f32 v241, v241, s62, v95
	v_mov_b32_e32 v242, 0
	v_mov_b32_e32 v243, 0
	v_mov_b32_e32 v244, 0
	v_mov_b32_e32 v245, 0
	v_cvt_pk_fp8_f32 v242, v226, v227
	v_cvt_pk_fp8_f32 v243, v230, v231
	v_cvt_pk_fp8_f32 v244, v234, v235
	v_cvt_pk_fp8_f32 v245, v238, v239
	v_cvt_pk_fp8_f32 v242, v228, v229 op_sel:[0,0,1]
	v_cvt_pk_fp8_f32 v243, v232, v233 op_sel:[0,0,1]
	v_cvt_pk_fp8_f32 v244, v236, v237 op_sel:[0,0,1]
	v_cvt_pk_fp8_f32 v245, v240, v241 op_sel:[0,0,1]
	s_nop 0
	global_store_dwordx4 v80, v[242:245], s[6:7]
	s_waitcnt vmcnt(12)
	v_mul_f32_e32 v176, 0x43000000, v176
	v_mul_f32_e32 v177, 0x43000000, v177
	v_mul_f32_e32 v178, 0x43000000, v178
	v_mul_f32_e32 v179, 0x43000000, v179
	ds_write_b128 v210, v[176:179]
	v_mul_f32_e32 v180, 0x43000000, v180
	v_mul_f32_e32 v181, 0x43000000, v181
	v_mul_f32_e32 v182, 0x43000000, v182
	v_mul_f32_e32 v183, 0x43000000, v183
	ds_write_b128 v210, v[180:183] offset:1024
	v_mul_f32_e32 v184, 0x43000000, v184
	v_mul_f32_e32 v185, 0x43000000, v185
	v_mul_f32_e32 v186, 0x43000000, v186
	v_mul_f32_e32 v187, 0x43000000, v187
	ds_write_b128 v210, v[184:187] offset:2048
	v_mul_f32_e32 v188, 0x43000000, v188
	v_mul_f32_e32 v189, 0x43000000, v189
	v_mul_f32_e32 v190, 0x43000000, v190
	v_mul_f32_e32 v191, 0x43000000, v191
	ds_write_b128 v210, v[188:191] offset:3072
	v_mul_f32_e32 v192, 0x43000000, v192
	v_mul_f32_e32 v193, 0x43000000, v193
	v_mul_f32_e32 v194, 0x43000000, v194
	v_mul_f32_e32 v195, 0x43000000, v195
	ds_write_b128 v210, v[192:195] offset:4096
	v_mul_f32_e32 v196, 0x43000000, v196
	v_mul_f32_e32 v197, 0x43000000, v197
	v_mul_f32_e32 v198, 0x43000000, v198
	v_mul_f32_e32 v199, 0x43000000, v199
	ds_write_b128 v210, v[196:199] offset:5120
	v_mul_f32_e32 v200, 0x43000000, v200
	v_mul_f32_e32 v201, 0x43000000, v201
	v_mul_f32_e32 v202, 0x43000000, v202
	v_mul_f32_e32 v203, 0x43000000, v203
	ds_write_b128 v210, v[200:203] offset:6144
	v_mul_f32_e32 v204, 0x43000000, v204
	v_mul_f32_e32 v205, 0x43000000, v205
	v_mul_f32_e32 v206, 0x43000000, v206
	v_mul_f32_e32 v207, 0x43000000, v207
	ds_write_b128 v210, v[204:207] offset:7168
	s_waitcnt lgkmcnt(0)
	s_barrier
; #define GAS __attribute__((address_space(1)))
; #define LAS __attribute__((address_space(3)))
; #define LDS_WAIT() asm volatile("s_waitcnt lgkmcnt(0)" ::: "memory")
; __device__ __forceinline__ unsigned pk4_fp8(float a, float b, float c, float d) {
;     a = fminf(fmaxf(a, -448.f), 448.f); b = fminf(fmaxf(b, -448.f), 448.f); c = fminf(fmaxf(c, -448.f), 448.f); d = fminf(fmaxf(d, -448.f), 448.f);
;     int w = __builtin_amdgcn_cvt_pk_fp8_f32(a, b, 0, false); w = __builtin_amdgcn_cvt_pk_fp8_f32(c, d, w, true); return (unsigned)w; }
;     ...
; #pragma unroll
;     for (int i = 0; i < 32; ++i) v[i] = sc >= 0 ? W[(size_t)(k0 + 2 * i + (lane >> 5)) * Nsrc + sc] : 0.f;
; #pragma unroll
;     for (int i = 0; i < 32; ++i) { const int k = k0 + 2 * i + (lane >> 5); float x = v[i] * wscale; if (KS) x *= (k < ksplit ? ksA[k] : ksB[k - ksplit]); scr[(2 * i + (lane >> 5)) * 33 + (lane & 31)] = x; }
;     LDS_WAIT(); asm volatile("" ::: "memory");
;     const int c = lane & 7;
; #pragma unroll
;     for (int j = 0; j < 4; ++j) { const int n = (lane >> 3) + 8 * j; const LAS float* s = scr + (8 * c) * 33 + n;
;         const unsigned long long o = (unsigned long long)pg8::pk4_fp8(s[0 * 33], s[1 * 33], s[2 * 33], s[3 * 33]) | ((unsigned long long)pg8::pk4_fp8(s[4 * 33], s[5 * 33], s[6 * 33], s[7 * 33]) << 32);
;         *(GAS unsigned long long*)(WT + (size_t)(n0 + n) * K + k0 + 8 * c) = o; }
;     LDS_WAIT(); asm volatile("" ::: "memory");
	s_add_u32 s8, s38, 0x4003000
	s_addc_u32 s9, s39, 0
	global_load_dwordx4 v[176:179], v75, s[8:9]
	s_add_u32 s8, s8, 0x8000
	s_addc_u32 s9, s9, 0
	global_load_dwordx4 v[180:183], v75, s[8:9]
	s_add_u32 s8, s8, 0x8000
	s_addc_u32 s9, s9, 0
	global_load_dwordx4 v[184:187], v75, s[8:9]
	s_add_u32 s8, s8, 0x8000
	s_addc_u32 s9, s9, 0
	global_load_dwordx4 v[188:191], v75, s[8:9]
	s_add_u32 s8, s8, 0x8000
	s_addc_u32 s9, s9, 0
	global_load_dwordx4 v[192:195], v75, s[8:9]
	s_add_u32 s8, s8, 0x8000
	s_addc_u32 s9, s9, 0
	global_load_dwordx4 v[196:199], v75, s[8:9]
	s_add_u32 s8, s8, 0x8000
	s_addc_u32 s9, s9, 0
	global_load_dwordx4 v[200:203], v75, s[8:9]
	s_add_u32 s8, s8, 0x8000
	s_addc_u32 s9, s9, 0
	global_load_dwordx4 v[204:207], v75, s[8:9]
	s_add_u32 s6, s40, 0x1001000
	s_addc_u32 s7, s41, 0
	ds_read_b32 v226, v212
	ds_read_b32 v227, v212 offset:512
	ds_read_b32 v228, v212 offset:1024
	ds_read_b32 v229, v212 offset:1536
	ds_read_b32 v230, v212 offset:2048
	ds_read_b32 v231, v212 offset:2560
	ds_read_b32 v232, v212 offset:3072
	ds_read_b32 v233, v212 offset:3584
	ds_read_b32 v234, v212 offset:4096
	ds_read_b32 v235, v212 offset:4608
	ds_read_b32 v236, v212 offset:5120
	ds_read_b32 v237, v212 offset:5632
	ds_read_b32 v238, v212 offset:6144
	ds_read_b32 v239, v212 offset:6656
	ds_read_b32 v240, v212 offset:7168
	ds_read_b32 v241, v212 offset:7680
	s_waitcnt lgkmcnt(0)
	v_max_f32_e32 v226, v226, v226
	v_max_f32_e32 v227, v227, v227
	v_max_f32_e32 v228, v228, v228
	v_max_f32_e32 v229, v229, v229
	v_max_f32_e32 v230, v230, v230
	v_max_f32_e32 v231, v231, v231
	v_max_f32_e32 v232, v232, v232
	v_max_f32_e32 v233, v233, v233
	v_max_f32_e32 v234, v234, v234
	v_max_f32_e32 v235, v235, v235
	v_max_f32_e32 v236, v236, v236
	v_max_f32_e32 v237, v237, v237
	v_max_f32_e32 v238, v238, v238
	v_max_f32_e32 v239, v239, v239
	v_max_f32_e32 v240, v240, v240
	v_max_f32_e32 v241, v241, v241
	v_med3_f32 v226, v226, s62, v95
	v_med3_f32 v227, v227, s62, v95
	v_med3_f32 v228, v228, s62, v95
	v_med3_f32 v229, v229, s62, v95
	v_med3_f32 v230, v230, s62, v95
	v_med3_f32 v231, v231, s62, v95
	v_med3_f32 v232, v232, s62, v95
	v_med3_f32 v233, v233, s62, v95
	v_med3_f32 v234, v234, s62, v95
	v_med3_f32 v235, v235, s62, v95
	v_med3_f32 v236, v236, s62, v95
	v_med3_f32 v237, v237, s62, v95
	v_med3_f32 v238, v238, s62, v95
	v_med3_f32 v239, v239, s62, v95
	v_med3_f32 v240, v240, s62, v95
	v_med3_f32 v241, v241, s62, v95
	v_mov_b32_e32 v242, 0
	v_mov_b32_e32 v243, 0
	v_mov_b32_e32 v244, 0
	v_mov_b32_e32 v245, 0
	v_cvt_pk_fp8_f32 v242, v226, v227
	v_cvt_pk_fp8_f32 v243, v230, v231
	v_cvt_pk_fp8_f32 v244, v234, v235
	v_cvt_pk_fp8_f32 v245, v238, v239
	v_cvt_pk_fp8_f32 v242, v228, v229 op_sel:[0,0,1]
	v_cvt_pk_fp8_f32 v243, v232, v233 op_sel:[0,0,1]
	v_cvt_pk_fp8_f32 v244, v236, v237 op_sel:[0,0,1]
	v_cvt_pk_fp8_f32 v245, v240, v241 op_sel:[0,0,1]
	s_nop 0
	global_store_dwordx4 v79, v[242:245], s[6:7]
	ds_read_b32 v226, v214
	ds_read_b32 v227, v214 offset:512
	ds_read_b32 v228, v214 offset:1024
	ds_read_b32 v229, v214 offset:1536
	ds_read_b32 v230, v214 offset:2048
	ds_read_b32 v231, v214 offset:2560
	ds_read_b32 v232, v214 offset:3072
	ds_read_b32 v233, v214 offset:3584
	ds_read_b32 v234, v214 offset:4096
	ds_read_b32 v235, v214 offset:4608
	ds_read_b32 v236, v214 offset:5120
	ds_read_b32 v237, v214 offset:5632
	ds_read_b32 v238, v214 offset:6144
	ds_read_b32 v239, v214 offset:6656
	ds_read_b32 v240, v214 offset:7168
	ds_read_b32 v241, v214 offset:7680
	s_waitcnt lgkmcnt(0)
	v_max_f32_e32 v226, v226, v226
	v_max_f32_e32 v227, v227, v227
	v_max_f32_e32 v228, v228, v228
	v_max_f32_e32 v229, v229, v229
	v_max_f32_e32 v230, v230, v230
	v_max_f32_e32 v231, v231, v231
	v_max_f32_e32 v232, v232, v232
	v_max_f32_e32 v233, v233, v233
	v_max_f32_e32 v234, v234, v234
	v_max_f32_e32 v235, v235, v235
	v_max_f32_e32 v236, v236, v236
	v_max_f32_e32 v237, v237, v237
	v_max_f32_e32 v238, v238, v238
	v_max_f32_e32 v239, v239, v239
	v_max_f32_e32 v240, v240, v240
	v_max_f32_e32 v241, v241, v241
	v_med3_f32 v226, v226, s62, v95
	v_med3_f32 v227, v227, s62, v95
	v_med3_f32 v228, v228, s62, v95
	v_med3_f32 v229, v229, s62, v95
	v_med3_f32 v230, v230, s62, v95
	v_med3_f32 v231, v231, s62, v95
	v_med3_f32 v232, v232, s62, v95
	v_med3_f32 v233, v233, s62, v95
	v_med3_f32 v234, v234, s62, v95
	v_med3_f32 v235, v235, s62, v95
	v_med3_f32 v236, v236, s62, v95
	v_med3_f32 v237, v237, s62, v95
	v_med3_f32 v238, v238, s62, v95
	v_med3_f32 v239, v239, s62, v95
	v_med3_f32 v240, v240, s62, v95
	v_med3_f32 v241, v241, s62, v95
	v_mov_b32_e32 v242, 0
	v_mov_b32_e32 v243, 0
	v_mov_b32_e32 v244, 0
	v_mov_b32_e32 v245, 0
	v_cvt_pk_fp8_f32 v242, v226, v227
	v_cvt_pk_fp8_f32 v243, v230, v231
	v_cvt_pk_fp8_f32 v244, v234, v235
	v_cvt_pk_fp8_f32 v245, v238, v239
	v_cvt_pk_fp8_f32 v242, v228, v229 op_sel:[0,0,1]
	v_cvt_pk_fp8_f32 v243, v232, v233 op_sel:[0,0,1]
	v_cvt_pk_fp8_f32 v244, v236, v237 op_sel:[0,0,1]
	v_cvt_pk_fp8_f32 v245, v240, v241 op_sel:[0,0,1]
	s_nop 0
	global_store_dwordx4 v80, v[242:245], s[6:7]
	s_waitcnt vmcnt(12)
	v_mul_f32_e32 v144, 0x43000000, v144
	v_mul_f32_e32 v145, 0x43000000, v145
	v_mul_f32_e32 v146, 0x43000000, v146
	v_mul_f32_e32 v147, 0x43000000, v147
	ds_write_b128 v209, v[144:147]
	v_mul_f32_e32 v148, 0x43000000, v148
	v_mul_f32_e32 v149, 0x43000000, v149
	v_mul_f32_e32 v150, 0x43000000, v150
	v_mul_f32_e32 v151, 0x43000000, v151
	ds_write_b128 v209, v[148:151] offset:1024
	v_mul_f32_e32 v152, 0x43000000, v152
	v_mul_f32_e32 v153, 0x43000000, v153
	v_mul_f32_e32 v154, 0x43000000, v154
	v_mul_f32_e32 v155, 0x43000000, v155
	ds_write_b128 v209, v[152:155] offset:2048
	v_mul_f32_e32 v156, 0x43000000, v156
	v_mul_f32_e32 v157, 0x43000000, v157
	v_mul_f32_e32 v158, 0x43000000, v158
	v_mul_f32_e32 v159, 0x43000000, v159
	ds_write_b128 v209, v[156:159] offset:3072
	v_mul_f32_e32 v160, 0x43000000, v160
	v_mul_f32_e32 v161, 0x43000000, v161
	v_mul_f32_e32 v162, 0x43000000, v162
	v_mul_f32_e32 v163, 0x43000000, v163
	ds_write_b128 v209, v[160:163] offset:4096
	v_mul_f32_e32 v164, 0x43000000, v164
	v_mul_f32_e32 v165, 0x43000000, v165
	v_mul_f32_e32 v166, 0x43000000, v166
	v_mul_f32_e32 v167, 0x43000000, v167
	ds_write_b128 v209, v[164:167] offset:5120
	v_mul_f32_e32 v168, 0x43000000, v168
	v_mul_f32_e32 v169, 0x43000000, v169
	v_mul_f32_e32 v170, 0x43000000, v170
	v_mul_f32_e32 v171, 0x43000000, v171
	ds_write_b128 v209, v[168:171] offset:6144
	v_mul_f32_e32 v172, 0x43000000, v172
	v_mul_f32_e32 v173, 0x43000000, v173
	v_mul_f32_e32 v174, 0x43000000, v174
	v_mul_f32_e32 v175, 0x43000000, v175
	ds_write_b128 v209, v[172:175] offset:7168
	s_waitcnt lgkmcnt(0)
	s_barrier
; #define GAS __attribute__((address_space(1)))
; #define LAS __attribute__((address_space(3)))
; #define LDS_WAIT() asm volatile("s_waitcnt lgkmcnt(0)" ::: "memory")
; __device__ __forceinline__ unsigned pk4_fp8(float a, float b, float c, float d) {
;     a = fminf(fmaxf(a, -448.f), 448.f); b = fminf(fmaxf(b, -448.f), 448.f); c = fminf(fmaxf(c, -448.f), 448.f); d = fminf(fmaxf(d, -448.f), 448.f);
;     int w = __builtin_amdgcn_cvt_pk_fp8_f32(a, b, 0, false); w = __builtin_amdgcn_cvt_pk_fp8_f32(c, d, w, true); return (unsigned)w; }
;     ...
; #pragma unroll
;     for (int i = 0; i < 32; ++i) v[i] = sc >= 0 ? W[(size_t)(k0 + 2 * i + (lane >> 5)) * Nsrc + sc] : 0.f;
; #pragma unroll
;     for (int i = 0; i < 32; ++i) { const int k = k0 + 2 * i + (lane >> 5); float x = v[i] * wscale; if (KS) x *= (k < ksplit ? ksA[k] : ksB[k - ksplit]); scr[(2 * i + (lane >> 5)) * 33 + (lane & 31)] = x; }
;     LDS_WAIT(); asm volatile("" ::: "memory");
;     const int c = lane & 7;
; #pragma unroll
;     for (int j = 0; j < 4; ++j) { const int n = (lane >> 3) + 8 * j; const LAS float* s = scr + (8 * c) * 33 + n;
;         const unsigned long long o = (unsigned long long)pg8::pk4_fp8(s[0 * 33], s[1 * 33], s[2 * 33], s[3 * 33]) | ((unsigned long long)pg8::pk4_fp8(s[4 * 33], s[5 * 33], s[6 * 33], s[7 * 33]) << 32);
;         *(GAS unsigned long long*)(WT + (size_t)(n0 + n) * K + k0 + 8 * c) = o; }
;     LDS_WAIT(); asm volatile("" ::: "memory");
	s_add_u32 s8, s38, 0x8000000
	s_addc_u32 s9, s39, 0
	global_load_dwordx4 v[144:147], v75, s[8:9]
	s_add_u32 s8, s8, 0x8000
	s_addc_u32 s9, s9, 0
	global_load_dwordx4 v[148:151], v75, s[8:9]
	s_add_u32 s8, s8, 0x8000
	s_addc_u32 s9, s9, 0
	global_load_dwordx4 v[152:155], v75, s[8:9]
	s_add_u32 s8, s8, 0x8000
	s_addc_u32 s9, s9, 0
	global_load_dwordx4 v[156:159], v75, s[8:9]
	s_add_u32 s8, s8, 0x8000
	s_addc_u32 s9, s9, 0
	global_load_dwordx4 v[160:163], v75, s[8:9]
	s_add_u32 s8, s8, 0x8000
	s_addc_u32 s9, s9, 0
	global_load_dwordx4 v[164:167], v75, s[8:9]
	s_add_u32 s8, s8, 0x8000
	s_addc_u32 s9, s9, 0
	global_load_dwordx4 v[168:171], v75, s[8:9]
	s_add_u32 s8, s8, 0x8000
	s_addc_u32 s9, s9, 0
	global_load_dwordx4 v[172:175], v75, s[8:9]
	s_add_u32 s6, s40, 0x2001000
	s_addc_u32 s7, s41, 0
	ds_read_b32 v226, v211
	ds_read_b32 v227, v211 offset:512
	ds_read_b32 v228, v211 offset:1024
	ds_read_b32 v229, v211 offset:1536
	ds_read_b32 v230, v211 offset:2048
	ds_read_b32 v231, v211 offset:2560
	ds_read_b32 v232, v211 offset:3072
	ds_read_b32 v233, v211 offset:3584
	ds_read_b32 v234, v211 offset:4096
	ds_read_b32 v235, v211 offset:4608
	ds_read_b32 v236, v211 offset:5120
	ds_read_b32 v237, v211 offset:5632
	ds_read_b32 v238, v211 offset:6144
	ds_read_b32 v239, v211 offset:6656
	ds_read_b32 v240, v211 offset:7168
	ds_read_b32 v241, v211 offset:7680
	s_waitcnt lgkmcnt(0)
	v_max_f32_e32 v226, v226, v226
	v_max_f32_e32 v227, v227, v227
	v_max_f32_e32 v228, v228, v228
	v_max_f32_e32 v229, v229, v229
	v_max_f32_e32 v230, v230, v230
	v_max_f32_e32 v231, v231, v231
	v_max_f32_e32 v232, v232, v232
	v_max_f32_e32 v233, v233, v233
	v_max_f32_e32 v234, v234, v234
	v_max_f32_e32 v235, v235, v235
	v_max_f32_e32 v236, v236, v236
	v_max_f32_e32 v237, v237, v237
	v_max_f32_e32 v238, v238, v238
	v_max_f32_e32 v239, v239, v239
	v_max_f32_e32 v240, v240, v240
	v_max_f32_e32 v241, v241, v241
	v_med3_f32 v226, v226, s62, v95
	v_med3_f32 v227, v227, s62, v95
	v_med3_f32 v228, v228, s62, v95
	v_med3_f32 v229, v229, s62, v95
	v_med3_f32 v230, v230, s62, v95
	v_med3_f32 v231, v231, s62, v95
	v_med3_f32 v232, v232, s62, v95
	v_med3_f32 v233, v233, s62, v95
	v_med3_f32 v234, v234, s62, v95
	v_med3_f32 v235, v235, s62, v95
	v_med3_f32 v236, v236, s62, v95
	v_med3_f32 v237, v237, s62, v95
	v_med3_f32 v238, v238, s62, v95
	v_med3_f32 v239, v239, s62, v95
	v_med3_f32 v240, v240, s62, v95
	v_med3_f32 v241, v241, s62, v95
	v_mov_b32_e32 v242, 0
	v_mov_b32_e32 v243, 0
	v_mov_b32_e32 v244, 0
	v_mov_b32_e32 v245, 0
	v_cvt_pk_fp8_f32 v242, v226, v227
	v_cvt_pk_fp8_f32 v243, v230, v231
	v_cvt_pk_fp8_f32 v244, v234, v235
	v_cvt_pk_fp8_f32 v245, v238, v239
	v_cvt_pk_fp8_f32 v242, v228, v229 op_sel:[0,0,1]
	v_cvt_pk_fp8_f32 v243, v232, v233 op_sel:[0,0,1]
	v_cvt_pk_fp8_f32 v244, v236, v237 op_sel:[0,0,1]
	v_cvt_pk_fp8_f32 v245, v240, v241 op_sel:[0,0,1]
	s_nop 0
	global_store_dwordx4 v79, v[242:245], s[6:7]
	ds_read_b32 v226, v213
	ds_read_b32 v227, v213 offset:512
	ds_read_b32 v228, v213 offset:1024
	ds_read_b32 v229, v213 offset:1536
	ds_read_b32 v230, v213 offset:2048
	ds_read_b32 v231, v213 offset:2560
	ds_read_b32 v232, v213 offset:3072
	ds_read_b32 v233, v213 offset:3584
	ds_read_b32 v234, v213 offset:4096
	ds_read_b32 v235, v213 offset:4608
	ds_read_b32 v236, v213 offset:5120
	ds_read_b32 v237, v213 offset:5632
	ds_read_b32 v238, v213 offset:6144
	ds_read_b32 v239, v213 offset:6656
	ds_read_b32 v240, v213 offset:7168
	ds_read_b32 v241, v213 offset:7680
	s_waitcnt lgkmcnt(0)
	v_max_f32_e32 v226, v226, v226
	v_max_f32_e32 v227, v227, v227
	v_max_f32_e32 v228, v228, v228
	v_max_f32_e32 v229, v229, v229
	v_max_f32_e32 v230, v230, v230
	v_max_f32_e32 v231, v231, v231
	v_max_f32_e32 v232, v232, v232
	v_max_f32_e32 v233, v233, v233
	v_max_f32_e32 v234, v234, v234
	v_max_f32_e32 v235, v235, v235
	v_max_f32_e32 v236, v236, v236
	v_max_f32_e32 v237, v237, v237
	v_max_f32_e32 v238, v238, v238
	v_max_f32_e32 v239, v239, v239
	v_max_f32_e32 v240, v240, v240
	v_max_f32_e32 v241, v241, v241
	v_med3_f32 v226, v226, s62, v95
	v_med3_f32 v227, v227, s62, v95
	v_med3_f32 v228, v228, s62, v95
	v_med3_f32 v229, v229, s62, v95
	v_med3_f32 v230, v230, s62, v95
	v_med3_f32 v231, v231, s62, v95
	v_med3_f32 v232, v232, s62, v95
	v_med3_f32 v233, v233, s62, v95
	v_med3_f32 v234, v234, s62, v95
	v_med3_f32 v235, v235, s62, v95
	v_med3_f32 v236, v236, s62, v95
	v_med3_f32 v237, v237, s62, v95
	v_med3_f32 v238, v238, s62, v95
	v_med3_f32 v239, v239, s62, v95
	v_med3_f32 v240, v240, s62, v95
	v_med3_f32 v241, v241, s62, v95
	v_mov_b32_e32 v242, 0
	v_mov_b32_e32 v243, 0
	v_mov_b32_e32 v244, 0
	v_mov_b32_e32 v245, 0
	v_cvt_pk_fp8_f32 v242, v226, v227
	v_cvt_pk_fp8_f32 v243, v230, v231
	v_cvt_pk_fp8_f32 v244, v234, v235
	v_cvt_pk_fp8_f32 v245, v238, v239
	v_cvt_pk_fp8_f32 v242, v228, v229 op_sel:[0,0,1]
	v_cvt_pk_fp8_f32 v243, v232, v233 op_sel:[0,0,1]
	v_cvt_pk_fp8_f32 v244, v236, v237 op_sel:[0,0,1]
	v_cvt_pk_fp8_f32 v245, v240, v241 op_sel:[0,0,1]
	s_nop 0
	global_store_dwordx4 v80, v[242:245], s[6:7]
	s_branch .Lco3_hop_skip

; #define GAS __attribute__((address_space(1)))
; #define LAS __attribute__((address_space(3)))
; #define LDS_WAIT() asm volatile("s_waitcnt lgkmcnt(0)" ::: "memory")
; __device__ __forceinline__ unsigned pk4_fp8(float a, float b, float c, float d) {
;     a = fminf(fmaxf(a, -448.f), 448.f); b = fminf(fmaxf(b, -448.f), 448.f); c = fminf(fmaxf(c, -448.f), 448.f); d = fminf(fmaxf(d, -448.f), 448.f);
;     int w = __builtin_amdgcn_cvt_pk_fp8_f32(a, b, 0, false); w = __builtin_amdgcn_cvt_pk_fp8_f32(c, d, w, true); return (unsigned)w; }
;     ...
; #pragma unroll
;     for (int i = 0; i < 32; ++i) v[i] = sc >= 0 ? W[(size_t)(k0 + 2 * i + (lane >> 5)) * Nsrc + sc] : 0.f;
; #pragma unroll
;     for (int i = 0; i < 32; ++i) { const int k = k0 + 2 * i + (lane >> 5); float x = v[i] * wscale; if (KS) x *= (k < ksplit ? ksA[k] : ksB[k - ksplit]); scr[(2 * i + (lane >> 5)) * 33 + (lane & 31)] = x; }
;     LDS_WAIT(); asm volatile("" ::: "memory");
;     const int c = lane & 7;
; #pragma unroll
;     for (int j = 0; j < 4; ++j) { const int n = (lane >> 3) + 8 * j; const LAS float* s = scr + (8 * c) * 33 + n;
;         const unsigned long long o = (unsigned long long)pg8::pk4_fp8(s[0 * 33], s[1 * 33], s[2 * 33], s[3 * 33]) | ((unsigned long long)pg8::pk4_fp8(s[4 * 33], s[5 * 33], s[6 * 33], s[7 * 33]) << 32);
;         *(GAS unsigned long long*)(WT + (size_t)(n0 + n) * K + k0 + 8 * c) = o; }
;     LDS_WAIT(); asm volatile("" ::: "memory");
.Lco3_hop_skip:
	s_waitcnt vmcnt(12)
	v_mul_f32_e32 v176, 0x43000000, v176
	v_mul_f32_e32 v177, 0x43000000, v177
	v_mul_f32_e32 v178, 0x43000000, v178
	v_mul_f32_e32 v179, 0x43000000, v179
	ds_write_b128 v210, v[176:179]
	v_mul_f32_e32 v180, 0x43000000, v180
	v_mul_f32_e32 v181, 0x43000000, v181
	v_mul_f32_e32 v182, 0x43000000, v182
	v_mul_f32_e32 v183, 0x43000000, v183
	ds_write_b128 v210, v[180:183] offset:1024
	v_mul_f32_e32 v184, 0x43000000, v184
	v_mul_f32_e32 v185, 0x43000000, v185
	v_mul_f32_e32 v186, 0x43000000, v186
	v_mul_f32_e32 v187, 0x43000000, v187
	ds_write_b128 v210, v[184:187] offset:2048
	v_mul_f32_e32 v188, 0x43000000, v188
	v_mul_f32_e32 v189, 0x43000000, v189
	v_mul_f32_e32 v190, 0x43000000, v190
	v_mul_f32_e32 v191, 0x43000000, v191
	ds_write_b128 v210, v[188:191] offset:3072
	v_mul_f32_e32 v192, 0x43000000, v192
	v_mul_f32_e32 v193, 0x43000000, v193
	v_mul_f32_e32 v194, 0x43000000, v194
	v_mul_f32_e32 v195, 0x43000000, v195
	ds_write_b128 v210, v[192:195] offset:4096
	v_mul_f32_e32 v196, 0x43000000, v196
	v_mul_f32_e32 v197, 0x43000000, v197
	v_mul_f32_e32 v198, 0x43000000, v198
	v_mul_f32_e32 v199, 0x43000000, v199
	ds_write_b128 v210, v[196:199] offset:5120
	v_mul_f32_e32 v200, 0x43000000, v200
	v_mul_f32_e32 v201, 0x43000000, v201
	v_mul_f32_e32 v202, 0x43000000, v202
	v_mul_f32_e32 v203, 0x43000000, v203
	ds_write_b128 v210, v[200:203] offset:6144
	v_mul_f32_e32 v204, 0x43000000, v204
	v_mul_f32_e32 v205, 0x43000000, v205
	v_mul_f32_e32 v206, 0x43000000, v206
	v_mul_f32_e32 v207, 0x43000000, v207
	ds_write_b128 v210, v[204:207] offset:7168
	s_waitcnt lgkmcnt(0)
	s_barrier
	s_add_u32 s8, s38, 0x8001000
	s_addc_u32 s9, s39, 0
	global_load_dwordx4 v[176:179], v75, s[8:9]
	s_add_u32 s8, s8, 0x8000
	s_addc_u32 s9, s9, 0
	global_load_dwordx4 v[180:183], v75, s[8:9]
	s_add_u32 s8, s8, 0x8000
	s_addc_u32 s9, s9, 0
	global_load_dwordx4 v[184:187], v75, s[8:9]
	s_add_u32 s8, s8, 0x8000
	s_addc_u32 s9, s9, 0
	global_load_dwordx4 v[188:191], v75, s[8:9]
	s_add_u32 s8, s8, 0x8000
	s_addc_u32 s9, s9, 0
	global_load_dwordx4 v[192:195], v75, s[8:9]
	s_add_u32 s8, s8, 0x8000
	s_addc_u32 s9, s9, 0
	global_load_dwordx4 v[196:199], v75, s[8:9]
	s_add_u32 s8, s8, 0x8000
	s_addc_u32 s9, s9, 0
	global_load_dwordx4 v[200:203], v75, s[8:9]
	s_add_u32 s8, s8, 0x8000
	s_addc_u32 s9, s9, 0
	global_load_dwordx4 v[204:207], v75, s[8:9]
	s_add_u32 s6, s40, 0x3001000
	s_addc_u32 s7, s41, 0
	ds_read_b32 v226, v212
	ds_read_b32 v227, v212 offset:512
	ds_read_b32 v228, v212 offset:1024
	ds_read_b32 v229, v212 offset:1536
	ds_read_b32 v230, v212 offset:2048
	ds_read_b32 v231, v212 offset:2560
	ds_read_b32 v232, v212 offset:3072
	ds_read_b32 v233, v212 offset:3584
	ds_read_b32 v234, v212 offset:4096
	ds_read_b32 v235, v212 offset:4608
	ds_read_b32 v236, v212 offset:5120
	ds_read_b32 v237, v212 offset:5632
	ds_read_b32 v238, v212 offset:6144
	ds_read_b32 v239, v212 offset:6656
	ds_read_b32 v240, v212 offset:7168
	ds_read_b32 v241, v212 offset:7680
	s_waitcnt lgkmcnt(0)
	v_max_f32_e32 v226, v226, v226
	v_max_f32_e32 v227, v227, v227
	v_max_f32_e32 v228, v228, v228
	v_max_f32_e32 v229, v229, v229
	v_max_f32_e32 v230, v230, v230
	v_max_f32_e32 v231, v231, v231
	v_max_f32_e32 v232, v232, v232
	v_max_f32_e32 v233, v233, v233
	v_max_f32_e32 v234, v234, v234
	v_max_f32_e32 v235, v235, v235
	v_max_f32_e32 v236, v236, v236
	v_max_f32_e32 v237, v237, v237
	v_max_f32_e32 v238, v238, v238
	v_max_f32_e32 v239, v239, v239
	v_max_f32_e32 v240, v240, v240
	v_max_f32_e32 v241, v241, v241
	v_med3_f32 v226, v226, s62, v95
	v_med3_f32 v227, v227, s62, v95
	v_med3_f32 v228, v228, s62, v95
	v_med3_f32 v229, v229, s62, v95
	v_med3_f32 v230, v230, s62, v95
	v_med3_f32 v231, v231, s62, v95
	v_med3_f32 v232, v232, s62, v95
	v_med3_f32 v233, v233, s62, v95
	v_med3_f32 v234, v234, s62, v95
	v_med3_f32 v235, v235, s62, v95
	v_med3_f32 v236, v236, s62, v95
	v_med3_f32 v237, v237, s62, v95
	v_med3_f32 v238, v238, s62, v95
	v_med3_f32 v239, v239, s62, v95
	v_med3_f32 v240, v240, s62, v95
	v_med3_f32 v241, v241, s62, v95
	v_mov_b32_e32 v242, 0
	v_mov_b32_e32 v243, 0
	v_mov_b32_e32 v244, 0
	v_mov_b32_e32 v245, 0
	v_cvt_pk_fp8_f32 v242, v226, v227
	v_cvt_pk_fp8_f32 v243, v230, v231
	v_cvt_pk_fp8_f32 v244, v234, v235
	v_cvt_pk_fp8_f32 v245, v238, v239
	v_cvt_pk_fp8_f32 v242, v228, v229 op_sel:[0,0,1]
	v_cvt_pk_fp8_f32 v243, v232, v233 op_sel:[0,0,1]
	v_cvt_pk_fp8_f32 v244, v236, v237 op_sel:[0,0,1]
	v_cvt_pk_fp8_f32 v245, v240, v241 op_sel:[0,0,1]
	s_nop 0
	global_store_dwordx4 v79, v[242:245], s[6:7]
	ds_read_b32 v226, v214
	ds_read_b32 v227, v214 offset:512
	ds_read_b32 v228, v214 offset:1024
	ds_read_b32 v229, v214 offset:1536
	ds_read_b32 v230, v214 offset:2048
	ds_read_b32 v231, v214 offset:2560
	ds_read_b32 v232, v214 offset:3072
	ds_read_b32 v233, v214 offset:3584
	ds_read_b32 v234, v214 offset:4096
	ds_read_b32 v235, v214 offset:4608
	ds_read_b32 v236, v214 offset:5120
	ds_read_b32 v237, v214 offset:5632
	ds_read_b32 v238, v214 offset:6144
	ds_read_b32 v239, v214 offset:6656
	ds_read_b32 v240, v214 offset:7168
	ds_read_b32 v241, v214 offset:7680
	s_waitcnt lgkmcnt(0)
; #define GAS __attribute__((address_space(1)))
; #define LAS __attribute__((address_space(3)))
; #define LDS_WAIT() asm volatile("s_waitcnt lgkmcnt(0)" ::: "memory")
; __device__ __forceinline__ unsigned pk4_fp8(float a, float b, float c, float d) {
;     a = fminf(fmaxf(a, -448.f), 448.f); b = fminf(fmaxf(b, -448.f), 448.f); c = fminf(fmaxf(c, -448.f), 448.f); d = fminf(fmaxf(d, -448.f), 448.f);
;     int w = __builtin_amdgcn_cvt_pk_fp8_f32(a, b, 0, false); w = __builtin_amdgcn_cvt_pk_fp8_f32(c, d, w, true); return (unsigned)w; }
;     ...
; #pragma unroll
;     for (int i = 0; i < 32; ++i) v[i] = sc >= 0 ? W[(size_t)(k0 + 2 * i + (lane >> 5)) * Nsrc + sc] : 0.f;
; #pragma unroll
;     for (int i = 0; i < 32; ++i) { const int k = k0 + 2 * i + (lane >> 5); float x = v[i] * wscale; if (KS) x *= (k < ksplit ? ksA[k] : ksB[k - ksplit]); scr[(2 * i + (lane >> 5)) * 33 + (lane & 31)] = x; }
;     LDS_WAIT(); asm volatile("" ::: "memory");
;     const int c = lane & 7;
; #pragma unroll
;     for (int j = 0; j < 4; ++j) { const int n = (lane >> 3) + 8 * j; const LAS float* s = scr + (8 * c) * 33 + n;
;         const unsigned long long o = (unsigned long long)pg8::pk4_fp8(s[0 * 33], s[1 * 33], s[2 * 33], s[3 * 33]) | ((unsigned long long)pg8::pk4_fp8(s[4 * 33], s[5 * 33], s[6 * 33], s[7 * 33]) << 32);
;         *(GAS unsigned long long*)(WT + (size_t)(n0 + n) * K + k0 + 8 * c) = o; }
;     LDS_WAIT(); asm volatile("" ::: "memory");
	v_max_f32_e32 v226, v226, v226
	v_max_f32_e32 v227, v227, v227
	v_max_f32_e32 v228, v228, v228
	v_max_f32_e32 v229, v229, v229
	v_max_f32_e32 v230, v230, v230
	v_max_f32_e32 v231, v231, v231
	v_max_f32_e32 v232, v232, v232
	v_max_f32_e32 v233, v233, v233
	v_max_f32_e32 v234, v234, v234
	v_max_f32_e32 v235, v235, v235
	v_max_f32_e32 v236, v236, v236
	v_max_f32_e32 v237, v237, v237
	v_max_f32_e32 v238, v238, v238
	v_max_f32_e32 v239, v239, v239
	v_max_f32_e32 v240, v240, v240
	v_max_f32_e32 v241, v241, v241
	v_med3_f32 v226, v226, s62, v95
	v_med3_f32 v227, v227, s62, v95
	v_med3_f32 v228, v228, s62, v95
	v_med3_f32 v229, v229, s62, v95
	v_med3_f32 v230, v230, s62, v95
	v_med3_f32 v231, v231, s62, v95
	v_med3_f32 v232, v232, s62, v95
	v_med3_f32 v233, v233, s62, v95
	v_med3_f32 v234, v234, s62, v95
	v_med3_f32 v235, v235, s62, v95
	v_med3_f32 v236, v236, s62, v95
	v_med3_f32 v237, v237, s62, v95
	v_med3_f32 v238, v238, s62, v95
	v_med3_f32 v239, v239, s62, v95
	v_med3_f32 v240, v240, s62, v95
	v_med3_f32 v241, v241, s62, v95
	v_mov_b32_e32 v242, 0
	v_mov_b32_e32 v243, 0
	v_mov_b32_e32 v244, 0
	v_mov_b32_e32 v245, 0
	v_cvt_pk_fp8_f32 v242, v226, v227
	v_cvt_pk_fp8_f32 v243, v230, v231
	v_cvt_pk_fp8_f32 v244, v234, v235
	v_cvt_pk_fp8_f32 v245, v238, v239
	v_cvt_pk_fp8_f32 v242, v228, v229 op_sel:[0,0,1]
	v_cvt_pk_fp8_f32 v243, v232, v233 op_sel:[0,0,1]
	v_cvt_pk_fp8_f32 v244, v236, v237 op_sel:[0,0,1]
	v_cvt_pk_fp8_f32 v245, v240, v241 op_sel:[0,0,1]
	s_nop 0
	global_store_dwordx4 v80, v[242:245], s[6:7]
	s_waitcnt vmcnt(12)
	v_mul_f32_e32 v144, 0x43000000, v144
	v_mul_f32_e32 v145, 0x43000000, v145
	v_mul_f32_e32 v146, 0x43000000, v146
	v_mul_f32_e32 v147, 0x43000000, v147
	ds_write_b128 v209, v[144:147]
	v_mul_f32_e32 v148, 0x43000000, v148
	v_mul_f32_e32 v149, 0x43000000, v149
	v_mul_f32_e32 v150, 0x43000000, v150
	v_mul_f32_e32 v151, 0x43000000, v151
	ds_write_b128 v209, v[148:151] offset:1024
	v_mul_f32_e32 v152, 0x43000000, v152
	v_mul_f32_e32 v153, 0x43000000, v153
	v_mul_f32_e32 v154, 0x43000000, v154
	v_mul_f32_e32 v155, 0x43000000, v155
	ds_write_b128 v209, v[152:155] offset:2048
	v_mul_f32_e32 v156, 0x43000000, v156
	v_mul_f32_e32 v157, 0x43000000, v157
	v_mul_f32_e32 v158, 0x43000000, v158
	v_mul_f32_e32 v159, 0x43000000, v159
	ds_write_b128 v209, v[156:159] offset:3072
	v_mul_f32_e32 v160, 0x43000000, v160
	v_mul_f32_e32 v161, 0x43000000, v161
	v_mul_f32_e32 v162, 0x43000000, v162
	v_mul_f32_e32 v163, 0x43000000, v163
	ds_write_b128 v209, v[160:163] offset:4096
	v_mul_f32_e32 v164, 0x43000000, v164
	v_mul_f32_e32 v165, 0x43000000, v165
	v_mul_f32_e32 v166, 0x43000000, v166
	v_mul_f32_e32 v167, 0x43000000, v167
	ds_write_b128 v209, v[164:167] offset:5120
	v_mul_f32_e32 v168, 0x43000000, v168
	v_mul_f32_e32 v169, 0x43000000, v169
	v_mul_f32_e32 v170, 0x43000000, v170
	v_mul_f32_e32 v171, 0x43000000, v171
	ds_write_b128 v209, v[168:171] offset:6144
	v_mul_f32_e32 v172, 0x43000000, v172
	v_mul_f32_e32 v173, 0x43000000, v173
	v_mul_f32_e32 v174, 0x43000000, v174
	v_mul_f32_e32 v175, 0x43000000, v175
	ds_write_b128 v209, v[172:175] offset:7168
	s_waitcnt lgkmcnt(0)
	s_barrier
	s_add_u32 s8, s38, 0x8002000
	s_addc_u32 s9, s39, 0
	global_load_dwordx4 v[144:147], v75, s[8:9]
	s_add_u32 s8, s8, 0x8000
	s_addc_u32 s9, s9, 0
	global_load_dwordx4 v[148:151], v75, s[8:9]
	s_add_u32 s8, s8, 0x8000
	s_addc_u32 s9, s9, 0
	global_load_dwordx4 v[152:155], v75, s[8:9]
	s_add_u32 s8, s8, 0x8000
	s_addc_u32 s9, s9, 0
	global_load_dwordx4 v[156:159], v75, s[8:9]
	s_add_u32 s8, s8, 0x8000
	s_addc_u32 s9, s9, 0
	global_load_dwordx4 v[160:163], v75, s[8:9]
	s_add_u32 s8, s8, 0x8000
	s_addc_u32 s9, s9, 0
	global_load_dwordx4 v[164:167], v75, s[8:9]
	s_add_u32 s8, s8, 0x8000
	s_addc_u32 s9, s9, 0
	global_load_dwordx4 v[168:171], v75, s[8:9]
	s_add_u32 s8, s8, 0x8000
	s_addc_u32 s9, s9, 0
	global_load_dwordx4 v[172:175], v75, s[8:9]
	s_add_u32 s6, s40, 0x2000
	s_addc_u32 s7, s41, 0
	ds_read_b32 v226, v211
	ds_read_b32 v227, v211 offset:512
	ds_read_b32 v228, v211 offset:1024
	ds_read_b32 v229, v211 offset:1536
	ds_read_b32 v230, v211 offset:2048
	ds_read_b32 v231, v211 offset:2560
	ds_read_b32 v232, v211 offset:3072
	ds_read_b32 v233, v211 offset:3584
	ds_read_b32 v234, v211 offset:4096
	ds_read_b32 v235, v211 offset:4608
	ds_read_b32 v236, v211 offset:5120
	ds_read_b32 v237, v211 offset:5632
	ds_read_b32 v238, v211 offset:6144
	ds_read_b32 v239, v211 offset:6656
	ds_read_b32 v240, v211 offset:7168
	ds_read_b32 v241, v211 offset:7680
	s_waitcnt lgkmcnt(0)
	v_max_f32_e32 v226, v226, v226
	v_max_f32_e32 v227, v227, v227
	v_max_f32_e32 v228, v228, v228
	v_max_f32_e32 v229, v229, v229
	v_max_f32_e32 v230, v230, v230
	v_max_f32_e32 v231, v231, v231
	v_max_f32_e32 v232, v232, v232
	v_max_f32_e32 v233, v233, v233
	v_max_f32_e32 v234, v234, v234
	v_max_f32_e32 v235, v235, v235
	v_max_f32_e32 v236, v236, v236
	v_max_f32_e32 v237, v237, v237
	v_max_f32_e32 v238, v238, v238
	v_max_f32_e32 v239, v239, v239
	v_max_f32_e32 v240, v240, v240
	v_max_f32_e32 v241, v241, v241
	v_med3_f32 v226, v226, s62, v95
	v_med3_f32 v227, v227, s62, v95
	v_med3_f32 v228, v228, s62, v95
	v_med3_f32 v229, v229, s62, v95
	v_med3_f32 v230, v230, s62, v95
	v_med3_f32 v231, v231, s62, v95
	v_med3_f32 v232, v232, s62, v95
	v_med3_f32 v233, v233, s62, v95
	v_med3_f32 v234, v234, s62, v95
	v_med3_f32 v235, v235, s62, v95
	v_med3_f32 v236, v236, s62, v95
	v_med3_f32 v237, v237, s62, v95
	v_med3_f32 v238, v238, s62, v95
	v_med3_f32 v239, v239, s62, v95
	v_med3_f32 v240, v240, s62, v95
	v_med3_f32 v241, v241, s62, v95
	v_mov_b32_e32 v242, 0
	v_mov_b32_e32 v243, 0
	v_mov_b32_e32 v244, 0
	v_mov_b32_e32 v245, 0
	v_cvt_pk_fp8_f32 v242, v226, v227
	v_cvt_pk_fp8_f32 v243, v230, v231
	v_cvt_pk_fp8_f32 v244, v234, v235
	v_cvt_pk_fp8_f32 v245, v238, v239
	v_cvt_pk_fp8_f32 v242, v228, v229 op_sel:[0,0,1]
	v_cvt_pk_fp8_f32 v243, v232, v233 op_sel:[0,0,1]
	v_cvt_pk_fp8_f32 v244, v236, v237 op_sel:[0,0,1]
	v_cvt_pk_fp8_f32 v245, v240, v241 op_sel:[0,0,1]
	s_nop 0
	global_store_dwordx4 v79, v[242:245], s[6:7]
	ds_read_b32 v226, v213
	ds_read_b32 v227, v213 offset:512
	ds_read_b32 v228, v213 offset:1024
	ds_read_b32 v229, v213 offset:1536
	ds_read_b32 v230, v213 offset:2048
	ds_read_b32 v231, v213 offset:2560
	ds_read_b32 v232, v213 offset:3072
	ds_read_b32 v233, v213 offset:3584
	ds_read_b32 v234, v213 offset:4096
	ds_read_b32 v235, v213 offset:4608
	ds_read_b32 v236, v213 offset:5120
	ds_read_b32 v237, v213 offset:5632
	ds_read_b32 v238, v213 offset:6144
	ds_read_b32 v239, v213 offset:6656
	ds_read_b32 v240, v213 offset:7168
	ds_read_b32 v241, v213 offset:7680
	s_waitcnt lgkmcnt(0)
; #define GAS __attribute__((address_space(1)))
; #define LAS __attribute__((address_space(3)))
; #define LDS_WAIT() asm volatile("s_waitcnt lgkmcnt(0)" ::: "memory")
; __device__ __forceinline__ unsigned pk4_fp8(float a, float b, float c, float d) {
;     a = fminf(fmaxf(a, -448.f), 448.f); b = fminf(fmaxf(b, -448.f), 448.f); c = fminf(fmaxf(c, -448.f), 448.f); d = fminf(fmaxf(d, -448.f), 448.f);
;     int w = __builtin_amdgcn_cvt_pk_fp8_f32(a, b, 0, false); w = __builtin_amdgcn_cvt_pk_fp8_f32(c, d, w, true); return (unsigned)w; }
;     ...
; #pragma unroll
;     for (int i = 0; i < 32; ++i) v[i] = sc >= 0 ? W[(size_t)(k0 + 2 * i + (lane >> 5)) * Nsrc + sc] : 0.f;
; #pragma unroll
;     for (int i = 0; i < 32; ++i) { const int k = k0 + 2 * i + (lane >> 5); float x = v[i] * wscale; if (KS) x *= (k < ksplit ? ksA[k] : ksB[k - ksplit]); scr[(2 * i + (lane >> 5)) * 33 + (lane & 31)] = x; }
;     LDS_WAIT(); asm volatile("" ::: "memory");
;     const int c = lane & 7;
; #pragma unroll
;     for (int j = 0; j < 4; ++j) { const int n = (lane >> 3) + 8 * j; const LAS float* s = scr + (8 * c) * 33 + n;
;         const unsigned long long o = (unsigned long long)pg8::pk4_fp8(s[0 * 33], s[1 * 33], s[2 * 33], s[3 * 33]) | ((unsigned long long)pg8::pk4_fp8(s[4 * 33], s[5 * 33], s[6 * 33], s[7 * 33]) << 32);
;         *(GAS unsigned long long*)(WT + (size_t)(n0 + n) * K + k0 + 8 * c) = o; }
;     LDS_WAIT(); asm volatile("" ::: "memory");
	v_max_f32_e32 v226, v226, v226
	v_max_f32_e32 v227, v227, v227
	v_max_f32_e32 v228, v228, v228
	v_max_f32_e32 v229, v229, v229
	v_max_f32_e32 v230, v230, v230
	v_max_f32_e32 v231, v231, v231
	v_max_f32_e32 v232, v232, v232
	v_max_f32_e32 v233, v233, v233
	v_max_f32_e32 v234, v234, v234
	v_max_f32_e32 v235, v235, v235
	v_max_f32_e32 v236, v236, v236
	v_max_f32_e32 v237, v237, v237
	v_max_f32_e32 v238, v238, v238
	v_max_f32_e32 v239, v239, v239
	v_max_f32_e32 v240, v240, v240
	v_max_f32_e32 v241, v241, v241
	v_med3_f32 v226, v226, s62, v95
	v_med3_f32 v227, v227, s62, v95
	v_med3_f32 v228, v228, s62, v95
	v_med3_f32 v229, v229, s62, v95
	v_med3_f32 v230, v230, s62, v95
	v_med3_f32 v231, v231, s62, v95
	v_med3_f32 v232, v232, s62, v95
	v_med3_f32 v233, v233, s62, v95
	v_med3_f32 v234, v234, s62, v95
	v_med3_f32 v235, v235, s62, v95
	v_med3_f32 v236, v236, s62, v95
	v_med3_f32 v237, v237, s62, v95
	v_med3_f32 v238, v238, s62, v95
	v_med3_f32 v239, v239, s62, v95
	v_med3_f32 v240, v240, s62, v95
	v_med3_f32 v241, v241, s62, v95
	v_mov_b32_e32 v242, 0
	v_mov_b32_e32 v243, 0
	v_mov_b32_e32 v244, 0
	v_mov_b32_e32 v245, 0
	v_cvt_pk_fp8_f32 v242, v226, v227
	v_cvt_pk_fp8_f32 v243, v230, v231
	v_cvt_pk_fp8_f32 v244, v234, v235
	v_cvt_pk_fp8_f32 v245, v238, v239
	v_cvt_pk_fp8_f32 v242, v228, v229 op_sel:[0,0,1]
	v_cvt_pk_fp8_f32 v243, v232, v233 op_sel:[0,0,1]
	v_cvt_pk_fp8_f32 v244, v236, v237 op_sel:[0,0,1]
	v_cvt_pk_fp8_f32 v245, v240, v241 op_sel:[0,0,1]
	s_nop 0
	global_store_dwordx4 v80, v[242:245], s[6:7]
	s_waitcnt vmcnt(12)
	v_mul_f32_e32 v176, 0x43000000, v176
	v_mul_f32_e32 v177, 0x43000000, v177
	v_mul_f32_e32 v178, 0x43000000, v178
	v_mul_f32_e32 v179, 0x43000000, v179
	ds_write_b128 v210, v[176:179]
	v_mul_f32_e32 v180, 0x43000000, v180
	v_mul_f32_e32 v181, 0x43000000, v181
	v_mul_f32_e32 v182, 0x43000000, v182
	v_mul_f32_e32 v183, 0x43000000, v183
	ds_write_b128 v210, v[180:183] offset:1024
	v_mul_f32_e32 v184, 0x43000000, v184
	v_mul_f32_e32 v185, 0x43000000, v185
	v_mul_f32_e32 v186, 0x43000000, v186
	v_mul_f32_e32 v187, 0x43000000, v187
	ds_write_b128 v210, v[184:187] offset:2048
	v_mul_f32_e32 v188, 0x43000000, v188
	v_mul_f32_e32 v189, 0x43000000, v189
	v_mul_f32_e32 v190, 0x43000000, v190
	v_mul_f32_e32 v191, 0x43000000, v191
	ds_write_b128 v210, v[188:191] offset:3072
	v_mul_f32_e32 v192, 0x43000000, v192
	v_mul_f32_e32 v193, 0x43000000, v193
	v_mul_f32_e32 v194, 0x43000000, v194
	v_mul_f32_e32 v195, 0x43000000, v195
	ds_write_b128 v210, v[192:195] offset:4096
	v_mul_f32_e32 v196, 0x43000000, v196
	v_mul_f32_e32 v197, 0x43000000, v197
	v_mul_f32_e32 v198, 0x43000000, v198
	v_mul_f32_e32 v199, 0x43000000, v199
	ds_write_b128 v210, v[196:199] offset:5120
	v_mul_f32_e32 v200, 0x43000000, v200
	v_mul_f32_e32 v201, 0x43000000, v201
	v_mul_f32_e32 v202, 0x43000000, v202
	v_mul_f32_e32 v203, 0x43000000, v203
	ds_write_b128 v210, v[200:203] offset:6144
	v_mul_f32_e32 v204, 0x43000000, v204
	v_mul_f32_e32 v205, 0x43000000, v205
	v_mul_f32_e32 v206, 0x43000000, v206
	v_mul_f32_e32 v207, 0x43000000, v207
	ds_write_b128 v210, v[204:207] offset:7168
	s_waitcnt lgkmcnt(0)
	s_barrier
	s_add_u32 s8, s38, 0x8003000
	s_addc_u32 s9, s39, 0
	global_load_dwordx4 v[176:179], v75, s[8:9]
	s_add_u32 s8, s8, 0x8000
	s_addc_u32 s9, s9, 0
	global_load_dwordx4 v[180:183], v75, s[8:9]
	s_add_u32 s8, s8, 0x8000
	s_addc_u32 s9, s9, 0
	global_load_dwordx4 v[184:187], v75, s[8:9]
	s_add_u32 s8, s8, 0x8000
	s_addc_u32 s9, s9, 0
	global_load_dwordx4 v[188:191], v75, s[8:9]
	s_add_u32 s8, s8, 0x8000
	s_addc_u32 s9, s9, 0
	global_load_dwordx4 v[192:195], v75, s[8:9]
	s_add_u32 s8, s8, 0x8000
	s_addc_u32 s9, s9, 0
	global_load_dwordx4 v[196:199], v75, s[8:9]
	s_add_u32 s8, s8, 0x8000
	s_addc_u32 s9, s9, 0
	global_load_dwordx4 v[200:203], v75, s[8:9]
	s_add_u32 s8, s8, 0x8000
	s_addc_u32 s9, s9, 0
	global_load_dwordx4 v[204:207], v75, s[8:9]
	s_add_u32 s6, s40, 0x1002000
	s_addc_u32 s7, s41, 0
	ds_read_b32 v226, v212
	ds_read_b32 v227, v212 offset:512
	ds_read_b32 v228, v212 offset:1024
	ds_read_b32 v229, v212 offset:1536
	ds_read_b32 v230, v212 offset:2048
	ds_read_b32 v231, v212 offset:2560
	ds_read_b32 v232, v212 offset:3072
	ds_read_b32 v233, v212 offset:3584
	ds_read_b32 v234, v212 offset:4096
	ds_read_b32 v235, v212 offset:4608
	ds_read_b32 v236, v212 offset:5120
	ds_read_b32 v237, v212 offset:5632
	ds_read_b32 v238, v212 offset:6144
	ds_read_b32 v239, v212 offset:6656
	ds_read_b32 v240, v212 offset:7168
	ds_read_b32 v241, v212 offset:7680
	s_waitcnt lgkmcnt(0)
	v_max_f32_e32 v226, v226, v226
	v_max_f32_e32 v227, v227, v227
	v_max_f32_e32 v228, v228, v228
	v_max_f32_e32 v229, v229, v229
	v_max_f32_e32 v230, v230, v230
	v_max_f32_e32 v231, v231, v231
	v_max_f32_e32 v232, v232, v232
	v_max_f32_e32 v233, v233, v233
	v_max_f32_e32 v234, v234, v234
	v_max_f32_e32 v235, v235, v235
	v_max_f32_e32 v236, v236, v236
	v_max_f32_e32 v237, v237, v237
	v_max_f32_e32 v238, v238, v238
	v_max_f32_e32 v239, v239, v239
	v_max_f32_e32 v240, v240, v240
	v_max_f32_e32 v241, v241, v241
	v_med3_f32 v226, v226, s62, v95
	v_med3_f32 v227, v227, s62, v95
	v_med3_f32 v228, v228, s62, v95
	v_med3_f32 v229, v229, s62, v95
	v_med3_f32 v230, v230, s62, v95
	v_med3_f32 v231, v231, s62, v95
	v_med3_f32 v232, v232, s62, v95
	v_med3_f32 v233, v233, s62, v95
	v_med3_f32 v234, v234, s62, v95
	v_med3_f32 v235, v235, s62, v95
	v_med3_f32 v236, v236, s62, v95
	v_med3_f32 v237, v237, s62, v95
	v_med3_f32 v238, v238, s62, v95
	v_med3_f32 v239, v239, s62, v95
	v_med3_f32 v240, v240, s62, v95
	v_med3_f32 v241, v241, s62, v95
	v_mov_b32_e32 v242, 0
	v_mov_b32_e32 v243, 0
	v_mov_b32_e32 v244, 0
	v_mov_b32_e32 v245, 0
	v_cvt_pk_fp8_f32 v242, v226, v227
	v_cvt_pk_fp8_f32 v243, v230, v231
	v_cvt_pk_fp8_f32 v244, v234, v235
	v_cvt_pk_fp8_f32 v245, v238, v239
	v_cvt_pk_fp8_f32 v242, v228, v229 op_sel:[0,0,1]
	v_cvt_pk_fp8_f32 v243, v232, v233 op_sel:[0,0,1]
	v_cvt_pk_fp8_f32 v244, v236, v237 op_sel:[0,0,1]
	v_cvt_pk_fp8_f32 v245, v240, v241 op_sel:[0,0,1]
	s_nop 0
	global_store_dwordx4 v79, v[242:245], s[6:7]
	ds_read_b32 v226, v214
	ds_read_b32 v227, v214 offset:512
	ds_read_b32 v228, v214 offset:1024
	ds_read_b32 v229, v214 offset:1536
	ds_read_b32 v230, v214 offset:2048
	ds_read_b32 v231, v214 offset:2560
	ds_read_b32 v232, v214 offset:3072
	ds_read_b32 v233, v214 offset:3584
	ds_read_b32 v234, v214 offset:4096
	ds_read_b32 v235, v214 offset:4608
	ds_read_b32 v236, v214 offset:5120
	ds_read_b32 v237, v214 offset:5632
	ds_read_b32 v238, v214 offset:6144
	ds_read_b32 v239, v214 offset:6656
	ds_read_b32 v240, v214 offset:7168
	ds_read_b32 v241, v214 offset:7680
	s_waitcnt lgkmcnt(0)
; #define GAS __attribute__((address_space(1)))
; #define LAS __attribute__((address_space(3)))
; #define LDS_WAIT() asm volatile("s_waitcnt lgkmcnt(0)" ::: "memory")
; __device__ __forceinline__ unsigned pk4_fp8(float a, float b, float c, float d) {
;     a = fminf(fmaxf(a, -448.f), 448.f); b = fminf(fmaxf(b, -448.f), 448.f); c = fminf(fmaxf(c, -448.f), 448.f); d = fminf(fmaxf(d, -448.f), 448.f);
;     int w = __builtin_amdgcn_cvt_pk_fp8_f32(a, b, 0, false); w = __builtin_amdgcn_cvt_pk_fp8_f32(c, d, w, true); return (unsigned)w; }
;     ...
; #pragma unroll
;     for (int i = 0; i < 32; ++i) v[i] = sc >= 0 ? W[(size_t)(k0 + 2 * i + (lane >> 5)) * Nsrc + sc] : 0.f;
; #pragma unroll
;     for (int i = 0; i < 32; ++i) { const int k = k0 + 2 * i + (lane >> 5); float x = v[i] * wscale; if (KS) x *= (k < ksplit ? ksA[k] : ksB[k - ksplit]); scr[(2 * i + (lane >> 5)) * 33 + (lane & 31)] = x; }
;     LDS_WAIT(); asm volatile("" ::: "memory");
;     const int c = lane & 7;
; #pragma unroll
;     for (int j = 0; j < 4; ++j) { const int n = (lane >> 3) + 8 * j; const LAS float* s = scr + (8 * c) * 33 + n;
;         const unsigned long long o = (unsigned long long)pg8::pk4_fp8(s[0 * 33], s[1 * 33], s[2 * 33], s[3 * 33]) | ((unsigned long long)pg8::pk4_fp8(s[4 * 33], s[5 * 33], s[6 * 33], s[7 * 33]) << 32);
;         *(GAS unsigned long long*)(WT + (size_t)(n0 + n) * K + k0 + 8 * c) = o; }
;     LDS_WAIT(); asm volatile("" ::: "memory");
	v_max_f32_e32 v226, v226, v226
	v_max_f32_e32 v227, v227, v227
	v_max_f32_e32 v228, v228, v228
	v_max_f32_e32 v229, v229, v229
	v_max_f32_e32 v230, v230, v230
	v_max_f32_e32 v231, v231, v231
	v_max_f32_e32 v232, v232, v232
	v_max_f32_e32 v233, v233, v233
	v_max_f32_e32 v234, v234, v234
	v_max_f32_e32 v235, v235, v235
	v_max_f32_e32 v236, v236, v236
	v_max_f32_e32 v237, v237, v237
	v_max_f32_e32 v238, v238, v238
	v_max_f32_e32 v239, v239, v239
	v_max_f32_e32 v240, v240, v240
	v_max_f32_e32 v241, v241, v241
	v_med3_f32 v226, v226, s62, v95
	v_med3_f32 v227, v227, s62, v95
	v_med3_f32 v228, v228, s62, v95
	v_med3_f32 v229, v229, s62, v95
	v_med3_f32 v230, v230, s62, v95
	v_med3_f32 v231, v231, s62, v95
	v_med3_f32 v232, v232, s62, v95
	v_med3_f32 v233, v233, s62, v95
	v_med3_f32 v234, v234, s62, v95
	v_med3_f32 v235, v235, s62, v95
	v_med3_f32 v236, v236, s62, v95
	v_med3_f32 v237, v237, s62, v95
	v_med3_f32 v238, v238, s62, v95
	v_med3_f32 v239, v239, s62, v95
	v_med3_f32 v240, v240, s62, v95
	v_med3_f32 v241, v241, s62, v95
	v_mov_b32_e32 v242, 0
	v_mov_b32_e32 v243, 0
	v_mov_b32_e32 v244, 0
	v_mov_b32_e32 v245, 0
	v_cvt_pk_fp8_f32 v242, v226, v227
	v_cvt_pk_fp8_f32 v243, v230, v231
	v_cvt_pk_fp8_f32 v244, v234, v235
	v_cvt_pk_fp8_f32 v245, v238, v239
	v_cvt_pk_fp8_f32 v242, v228, v229 op_sel:[0,0,1]
	v_cvt_pk_fp8_f32 v243, v232, v233 op_sel:[0,0,1]
	v_cvt_pk_fp8_f32 v244, v236, v237 op_sel:[0,0,1]
	v_cvt_pk_fp8_f32 v245, v240, v241 op_sel:[0,0,1]
	s_nop 0
	global_store_dwordx4 v80, v[242:245], s[6:7]
	s_waitcnt vmcnt(12)
	v_mul_f32_e32 v144, 0x43000000, v144
	v_mul_f32_e32 v145, 0x43000000, v145
	v_mul_f32_e32 v146, 0x43000000, v146
	v_mul_f32_e32 v147, 0x43000000, v147
	ds_write_b128 v209, v[144:147]
	v_mul_f32_e32 v148, 0x43000000, v148
	v_mul_f32_e32 v149, 0x43000000, v149
	v_mul_f32_e32 v150, 0x43000000, v150
	v_mul_f32_e32 v151, 0x43000000, v151
	ds_write_b128 v209, v[148:151] offset:1024
	v_mul_f32_e32 v152, 0x43000000, v152
	v_mul_f32_e32 v153, 0x43000000, v153
	v_mul_f32_e32 v154, 0x43000000, v154
	v_mul_f32_e32 v155, 0x43000000, v155
	ds_write_b128 v209, v[152:155] offset:2048
	v_mul_f32_e32 v156, 0x43000000, v156
	v_mul_f32_e32 v157, 0x43000000, v157
	v_mul_f32_e32 v158, 0x43000000, v158
	v_mul_f32_e32 v159, 0x43000000, v159
	ds_write_b128 v209, v[156:159] offset:3072
	v_mul_f32_e32 v160, 0x43000000, v160
	v_mul_f32_e32 v161, 0x43000000, v161
	v_mul_f32_e32 v162, 0x43000000, v162
	v_mul_f32_e32 v163, 0x43000000, v163
	ds_write_b128 v209, v[160:163] offset:4096
	v_mul_f32_e32 v164, 0x43000000, v164
	v_mul_f32_e32 v165, 0x43000000, v165
	v_mul_f32_e32 v166, 0x43000000, v166
	v_mul_f32_e32 v167, 0x43000000, v167
	ds_write_b128 v209, v[164:167] offset:5120
	v_mul_f32_e32 v168, 0x43000000, v168
	v_mul_f32_e32 v169, 0x43000000, v169
	v_mul_f32_e32 v170, 0x43000000, v170
	v_mul_f32_e32 v171, 0x43000000, v171
	ds_write_b128 v209, v[168:171] offset:6144
	v_mul_f32_e32 v172, 0x43000000, v172
	v_mul_f32_e32 v173, 0x43000000, v173
	v_mul_f32_e32 v174, 0x43000000, v174
	v_mul_f32_e32 v175, 0x43000000, v175
	ds_write_b128 v209, v[172:175] offset:7168
	s_waitcnt lgkmcnt(0)
	s_barrier
	s_add_u32 s8, s38, 0xc000000
	s_addc_u32 s9, s39, 0
	global_load_dwordx4 v[144:147], v75, s[8:9]
	s_add_u32 s8, s8, 0x8000
	s_addc_u32 s9, s9, 0
	global_load_dwordx4 v[148:151], v75, s[8:9]
	s_add_u32 s8, s8, 0x8000
	s_addc_u32 s9, s9, 0
	global_load_dwordx4 v[152:155], v75, s[8:9]
	s_add_u32 s8, s8, 0x8000
	s_addc_u32 s9, s9, 0
	global_load_dwordx4 v[156:159], v75, s[8:9]
	s_add_u32 s8, s8, 0x8000
	s_addc_u32 s9, s9, 0
	global_load_dwordx4 v[160:163], v75, s[8:9]
	s_add_u32 s8, s8, 0x8000
	s_addc_u32 s9, s9, 0
	global_load_dwordx4 v[164:167], v75, s[8:9]
	s_add_u32 s8, s8, 0x8000
	s_addc_u32 s9, s9, 0
	global_load_dwordx4 v[168:171], v75, s[8:9]
	s_add_u32 s8, s8, 0x8000
	s_addc_u32 s9, s9, 0
	global_load_dwordx4 v[172:175], v75, s[8:9]
	s_add_u32 s6, s40, 0x2002000
	s_addc_u32 s7, s41, 0
	ds_read_b32 v226, v211
	ds_read_b32 v227, v211 offset:512
	ds_read_b32 v228, v211 offset:1024
	ds_read_b32 v229, v211 offset:1536
	ds_read_b32 v230, v211 offset:2048
	ds_read_b32 v231, v211 offset:2560
	ds_read_b32 v232, v211 offset:3072
	ds_read_b32 v233, v211 offset:3584
	ds_read_b32 v234, v211 offset:4096
	ds_read_b32 v235, v211 offset:4608
	ds_read_b32 v236, v211 offset:5120
	ds_read_b32 v237, v211 offset:5632
	ds_read_b32 v238, v211 offset:6144
	ds_read_b32 v239, v211 offset:6656
	ds_read_b32 v240, v211 offset:7168
	ds_read_b32 v241, v211 offset:7680
	s_waitcnt lgkmcnt(0)
	v_max_f32_e32 v226, v226, v226
	v_max_f32_e32 v227, v227, v227
	v_max_f32_e32 v228, v228, v228
	v_max_f32_e32 v229, v229, v229
	v_max_f32_e32 v230, v230, v230
	v_max_f32_e32 v231, v231, v231
	v_max_f32_e32 v232, v232, v232
	v_max_f32_e32 v233, v233, v233
	v_max_f32_e32 v234, v234, v234
	v_max_f32_e32 v235, v235, v235
	v_max_f32_e32 v236, v236, v236
	v_max_f32_e32 v237, v237, v237
	v_max_f32_e32 v238, v238, v238
	v_max_f32_e32 v239, v239, v239
	v_max_f32_e32 v240, v240, v240
	v_max_f32_e32 v241, v241, v241
	v_med3_f32 v226, v226, s62, v95
	v_med3_f32 v227, v227, s62, v95
	v_med3_f32 v228, v228, s62, v95
	v_med3_f32 v229, v229, s62, v95
	v_med3_f32 v230, v230, s62, v95
	v_med3_f32 v231, v231, s62, v95
	v_med3_f32 v232, v232, s62, v95
	v_med3_f32 v233, v233, s62, v95
	v_med3_f32 v234, v234, s62, v95
	v_med3_f32 v235, v235, s62, v95
	v_med3_f32 v236, v236, s62, v95
	v_med3_f32 v237, v237, s62, v95
	v_med3_f32 v238, v238, s62, v95
	v_med3_f32 v239, v239, s62, v95
	v_med3_f32 v240, v240, s62, v95
	v_med3_f32 v241, v241, s62, v95
	v_mov_b32_e32 v242, 0
	v_mov_b32_e32 v243, 0
	v_mov_b32_e32 v244, 0
	v_mov_b32_e32 v245, 0
	v_cvt_pk_fp8_f32 v242, v226, v227
	v_cvt_pk_fp8_f32 v243, v230, v231
	v_cvt_pk_fp8_f32 v244, v234, v235
	v_cvt_pk_fp8_f32 v245, v238, v239
	v_cvt_pk_fp8_f32 v242, v228, v229 op_sel:[0,0,1]
	v_cvt_pk_fp8_f32 v243, v232, v233 op_sel:[0,0,1]
	v_cvt_pk_fp8_f32 v244, v236, v237 op_sel:[0,0,1]
	v_cvt_pk_fp8_f32 v245, v240, v241 op_sel:[0,0,1]
	s_nop 0
	global_store_dwordx4 v79, v[242:245], s[6:7]
	ds_read_b32 v226, v213
	ds_read_b32 v227, v213 offset:512
	ds_read_b32 v228, v213 offset:1024
	ds_read_b32 v229, v213 offset:1536
	ds_read_b32 v230, v213 offset:2048
	ds_read_b32 v231, v213 offset:2560
	ds_read_b32 v232, v213 offset:3072
	ds_read_b32 v233, v213 offset:3584
	ds_read_b32 v234, v213 offset:4096
	ds_read_b32 v235, v213 offset:4608
	ds_read_b32 v236, v213 offset:5120
	ds_read_b32 v237, v213 offset:5632
	ds_read_b32 v238, v213 offset:6144
	ds_read_b32 v239, v213 offset:6656
	ds_read_b32 v240, v213 offset:7168
	ds_read_b32 v241, v213 offset:7680
	s_waitcnt lgkmcnt(0)
; #define GAS __attribute__((address_space(1)))
; #define LAS __attribute__((address_space(3)))
; #define LDS_WAIT() asm volatile("s_waitcnt lgkmcnt(0)" ::: "memory")
; __device__ __forceinline__ unsigned pk4_fp8(float a, float b, float c, float d) {
;     a = fminf(fmaxf(a, -448.f), 448.f); b = fminf(fmaxf(b, -448.f), 448.f); c = fminf(fmaxf(c, -448.f), 448.f); d = fminf(fmaxf(d, -448.f), 448.f);
;     int w = __builtin_amdgcn_cvt_pk_fp8_f32(a, b, 0, false); w = __builtin_amdgcn_cvt_pk_fp8_f32(c, d, w, true); return (unsigned)w; }
;     ...
; #pragma unroll
;     for (int i = 0; i < 32; ++i) v[i] = sc >= 0 ? W[(size_t)(k0 + 2 * i + (lane >> 5)) * Nsrc + sc] : 0.f;
; #pragma unroll
;     for (int i = 0; i < 32; ++i) { const int k = k0 + 2 * i + (lane >> 5); float x = v[i] * wscale; if (KS) x *= (k < ksplit ? ksA[k] : ksB[k - ksplit]); scr[(2 * i + (lane >> 5)) * 33 + (lane & 31)] = x; }
;     LDS_WAIT(); asm volatile("" ::: "memory");
;     const int c = lane & 7;
; #pragma unroll
;     for (int j = 0; j < 4; ++j) { const int n = (lane >> 3) + 8 * j; const LAS float* s = scr + (8 * c) * 33 + n;
;         const unsigned long long o = (unsigned long long)pg8::pk4_fp8(s[0 * 33], s[1 * 33], s[2 * 33], s[3 * 33]) | ((unsigned long long)pg8::pk4_fp8(s[4 * 33], s[5 * 33], s[6 * 33], s[7 * 33]) << 32);
;         *(GAS unsigned long long*)(WT + (size_t)(n0 + n) * K + k0 + 8 * c) = o; }
;     LDS_WAIT(); asm volatile("" ::: "memory");
	v_max_f32_e32 v226, v226, v226
	v_max_f32_e32 v227, v227, v227
	v_max_f32_e32 v228, v228, v228
	v_max_f32_e32 v229, v229, v229
	v_max_f32_e32 v230, v230, v230
	v_max_f32_e32 v231, v231, v231
	v_max_f32_e32 v232, v232, v232
	v_max_f32_e32 v233, v233, v233
	v_max_f32_e32 v234, v234, v234
	v_max_f32_e32 v235, v235, v235
	v_max_f32_e32 v236, v236, v236
	v_max_f32_e32 v237, v237, v237
	v_max_f32_e32 v238, v238, v238
	v_max_f32_e32 v239, v239, v239
	v_max_f32_e32 v240, v240, v240
	v_max_f32_e32 v241, v241, v241
	v_med3_f32 v226, v226, s62, v95
	v_med3_f32 v227, v227, s62, v95
	v_med3_f32 v228, v228, s62, v95
	v_med3_f32 v229, v229, s62, v95
	v_med3_f32 v230, v230, s62, v95
	v_med3_f32 v231, v231, s62, v95
	v_med3_f32 v232, v232, s62, v95
	v_med3_f32 v233, v233, s62, v95
	v_med3_f32 v234, v234, s62, v95
	v_med3_f32 v235, v235, s62, v95
	v_med3_f32 v236, v236, s62, v95
	v_med3_f32 v237, v237, s62, v95
	v_med3_f32 v238, v238, s62, v95
	v_med3_f32 v239, v239, s62, v95
	v_med3_f32 v240, v240, s62, v95
	v_med3_f32 v241, v241, s62, v95
	v_mov_b32_e32 v242, 0
	v_mov_b32_e32 v243, 0
	v_mov_b32_e32 v244, 0
	v_mov_b32_e32 v245, 0
	v_cvt_pk_fp8_f32 v242, v226, v227
	v_cvt_pk_fp8_f32 v243, v230, v231
	v_cvt_pk_fp8_f32 v244, v234, v235
	v_cvt_pk_fp8_f32 v245, v238, v239
	v_cvt_pk_fp8_f32 v242, v228, v229 op_sel:[0,0,1]
	v_cvt_pk_fp8_f32 v243, v232, v233 op_sel:[0,0,1]
	v_cvt_pk_fp8_f32 v244, v236, v237 op_sel:[0,0,1]
	v_cvt_pk_fp8_f32 v245, v240, v241 op_sel:[0,0,1]
	s_nop 0
	global_store_dwordx4 v80, v[242:245], s[6:7]
	s_waitcnt vmcnt(12)
	v_mul_f32_e32 v176, 0x43000000, v176
	v_mul_f32_e32 v177, 0x43000000, v177
	v_mul_f32_e32 v178, 0x43000000, v178
	v_mul_f32_e32 v179, 0x43000000, v179
	ds_write_b128 v210, v[176:179]
	v_mul_f32_e32 v180, 0x43000000, v180
	v_mul_f32_e32 v181, 0x43000000, v181
	v_mul_f32_e32 v182, 0x43000000, v182
	v_mul_f32_e32 v183, 0x43000000, v183
	ds_write_b128 v210, v[180:183] offset:1024
	v_mul_f32_e32 v184, 0x43000000, v184
	v_mul_f32_e32 v185, 0x43000000, v185
	v_mul_f32_e32 v186, 0x43000000, v186
	v_mul_f32_e32 v187, 0x43000000, v187
	ds_write_b128 v210, v[184:187] offset:2048
	v_mul_f32_e32 v188, 0x43000000, v188
	v_mul_f32_e32 v189, 0x43000000, v189
	v_mul_f32_e32 v190, 0x43000000, v190
	v_mul_f32_e32 v191, 0x43000000, v191
	ds_write_b128 v210, v[188:191] offset:3072
	v_mul_f32_e32 v192, 0x43000000, v192
	v_mul_f32_e32 v193, 0x43000000, v193
	v_mul_f32_e32 v194, 0x43000000, v194
	v_mul_f32_e32 v195, 0x43000000, v195
	ds_write_b128 v210, v[192:195] offset:4096
	v_mul_f32_e32 v196, 0x43000000, v196
	v_mul_f32_e32 v197, 0x43000000, v197
	v_mul_f32_e32 v198, 0x43000000, v198
	v_mul_f32_e32 v199, 0x43000000, v199
	ds_write_b128 v210, v[196:199] offset:5120
	v_mul_f32_e32 v200, 0x43000000, v200
	v_mul_f32_e32 v201, 0x43000000, v201
	v_mul_f32_e32 v202, 0x43000000, v202
	v_mul_f32_e32 v203, 0x43000000, v203
	ds_write_b128 v210, v[200:203] offset:6144
	v_mul_f32_e32 v204, 0x43000000, v204
	v_mul_f32_e32 v205, 0x43000000, v205
	v_mul_f32_e32 v206, 0x43000000, v206
	v_mul_f32_e32 v207, 0x43000000, v207
	ds_write_b128 v210, v[204:207] offset:7168
	s_waitcnt lgkmcnt(0)
	s_barrier
	s_add_u32 s8, s38, 0xc001000
	s_addc_u32 s9, s39, 0
	global_load_dwordx4 v[176:179], v75, s[8:9]
	s_add_u32 s8, s8, 0x8000
	s_addc_u32 s9, s9, 0
	global_load_dwordx4 v[180:183], v75, s[8:9]
	s_add_u32 s8, s8, 0x8000
	s_addc_u32 s9, s9, 0
	global_load_dwordx4 v[184:187], v75, s[8:9]
	s_add_u32 s8, s8, 0x8000
	s_addc_u32 s9, s9, 0
	global_load_dwordx4 v[188:191], v75, s[8:9]
	s_add_u32 s8, s8, 0x8000
	s_addc_u32 s9, s9, 0
	global_load_dwordx4 v[192:195], v75, s[8:9]
	s_add_u32 s8, s8, 0x8000
	s_addc_u32 s9, s9, 0
	global_load_dwordx4 v[196:199], v75, s[8:9]
	s_add_u32 s8, s8, 0x8000
	s_addc_u32 s9, s9, 0
	global_load_dwordx4 v[200:203], v75, s[8:9]
	s_add_u32 s8, s8, 0x8000
	s_addc_u32 s9, s9, 0
	global_load_dwordx4 v[204:207], v75, s[8:9]
	s_add_u32 s6, s40, 0x3002000
	s_addc_u32 s7, s41, 0
	ds_read_b32 v226, v212
	ds_read_b32 v227, v212 offset:512
	ds_read_b32 v228, v212 offset:1024
	ds_read_b32 v229, v212 offset:1536
	ds_read_b32 v230, v212 offset:2048
	ds_read_b32 v231, v212 offset:2560
	ds_read_b32 v232, v212 offset:3072
	ds_read_b32 v233, v212 offset:3584
	ds_read_b32 v234, v212 offset:4096
	ds_read_b32 v235, v212 offset:4608
	ds_read_b32 v236, v212 offset:5120
	ds_read_b32 v237, v212 offset:5632
	ds_read_b32 v238, v212 offset:6144
	ds_read_b32 v239, v212 offset:6656
	ds_read_b32 v240, v212 offset:7168
	ds_read_b32 v241, v212 offset:7680
	s_waitcnt lgkmcnt(0)
	v_max_f32_e32 v226, v226, v226
	v_max_f32_e32 v227, v227, v227
	v_max_f32_e32 v228, v228, v228
	v_max_f32_e32 v229, v229, v229
	v_max_f32_e32 v230, v230, v230
	v_max_f32_e32 v231, v231, v231
	v_max_f32_e32 v232, v232, v232
	v_max_f32_e32 v233, v233, v233
	v_max_f32_e32 v234, v234, v234
	v_max_f32_e32 v235, v235, v235
	v_max_f32_e32 v236, v236, v236
	v_max_f32_e32 v237, v237, v237
	v_max_f32_e32 v238, v238, v238
	v_max_f32_e32 v239, v239, v239
	v_max_f32_e32 v240, v240, v240
	v_max_f32_e32 v241, v241, v241
	v_med3_f32 v226, v226, s62, v95
	v_med3_f32 v227, v227, s62, v95
	v_med3_f32 v228, v228, s62, v95
	v_med3_f32 v229, v229, s62, v95
	v_med3_f32 v230, v230, s62, v95
	v_med3_f32 v231, v231, s62, v95
	v_med3_f32 v232, v232, s62, v95
	v_med3_f32 v233, v233, s62, v95
	v_med3_f32 v234, v234, s62, v95
	v_med3_f32 v235, v235, s62, v95
	v_med3_f32 v236, v236, s62, v95
	v_med3_f32 v237, v237, s62, v95
	v_med3_f32 v238, v238, s62, v95
	v_med3_f32 v239, v239, s62, v95
	v_med3_f32 v240, v240, s62, v95
	v_med3_f32 v241, v241, s62, v95
	v_mov_b32_e32 v242, 0
	v_mov_b32_e32 v243, 0
	v_mov_b32_e32 v244, 0
	v_mov_b32_e32 v245, 0
	v_cvt_pk_fp8_f32 v242, v226, v227
	v_cvt_pk_fp8_f32 v243, v230, v231
	v_cvt_pk_fp8_f32 v244, v234, v235
	v_cvt_pk_fp8_f32 v245, v238, v239
	v_cvt_pk_fp8_f32 v242, v228, v229 op_sel:[0,0,1]
	v_cvt_pk_fp8_f32 v243, v232, v233 op_sel:[0,0,1]
	v_cvt_pk_fp8_f32 v244, v236, v237 op_sel:[0,0,1]
	v_cvt_pk_fp8_f32 v245, v240, v241 op_sel:[0,0,1]
	s_nop 0
	global_store_dwordx4 v79, v[242:245], s[6:7]
	ds_read_b32 v226, v214
	ds_read_b32 v227, v214 offset:512
	ds_read_b32 v228, v214 offset:1024
	ds_read_b32 v229, v214 offset:1536
	ds_read_b32 v230, v214 offset:2048
	ds_read_b32 v231, v214 offset:2560
	ds_read_b32 v232, v214 offset:3072
	ds_read_b32 v233, v214 offset:3584
	ds_read_b32 v234, v214 offset:4096
	ds_read_b32 v235, v214 offset:4608
	ds_read_b32 v236, v214 offset:5120
	ds_read_b32 v237, v214 offset:5632
	ds_read_b32 v238, v214 offset:6144
	ds_read_b32 v239, v214 offset:6656
	ds_read_b32 v240, v214 offset:7168
	ds_read_b32 v241, v214 offset:7680
	s_waitcnt lgkmcnt(0)
; #define GAS __attribute__((address_space(1)))
; #define LAS __attribute__((address_space(3)))
; #define LDS_WAIT() asm volatile("s_waitcnt lgkmcnt(0)" ::: "memory")
; __device__ __forceinline__ unsigned pk4_fp8(float a, float b, float c, float d) {
;     a = fminf(fmaxf(a, -448.f), 448.f); b = fminf(fmaxf(b, -448.f), 448.f); c = fminf(fmaxf(c, -448.f), 448.f); d = fminf(fmaxf(d, -448.f), 448.f);
;     int w = __builtin_amdgcn_cvt_pk_fp8_f32(a, b, 0, false); w = __builtin_amdgcn_cvt_pk_fp8_f32(c, d, w, true); return (unsigned)w; }
;     ...
; #pragma unroll
;     for (int i = 0; i < 32; ++i) v[i] = sc >= 0 ? W[(size_t)(k0 + 2 * i + (lane >> 5)) * Nsrc + sc] : 0.f;
; #pragma unroll
;     for (int i = 0; i < 32; ++i) { const int k = k0 + 2 * i + (lane >> 5); float x = v[i] * wscale; if (KS) x *= (k < ksplit ? ksA[k] : ksB[k - ksplit]); scr[(2 * i + (lane >> 5)) * 33 + (lane & 31)] = x; }
;     LDS_WAIT(); asm volatile("" ::: "memory");
;     const int c = lane & 7;
; #pragma unroll
;     for (int j = 0; j < 4; ++j) { const int n = (lane >> 3) + 8 * j; const LAS float* s = scr + (8 * c) * 33 + n;
;         const unsigned long long o = (unsigned long long)pg8::pk4_fp8(s[0 * 33], s[1 * 33], s[2 * 33], s[3 * 33]) | ((unsigned long long)pg8::pk4_fp8(s[4 * 33], s[5 * 33], s[6 * 33], s[7 * 33]) << 32);
;         *(GAS unsigned long long*)(WT + (size_t)(n0 + n) * K + k0 + 8 * c) = o; }
;     LDS_WAIT(); asm volatile("" ::: "memory");
	v_max_f32_e32 v226, v226, v226
	v_max_f32_e32 v227, v227, v227
	v_max_f32_e32 v228, v228, v228
	v_max_f32_e32 v229, v229, v229
	v_max_f32_e32 v230, v230, v230
	v_max_f32_e32 v231, v231, v231
	v_max_f32_e32 v232, v232, v232
	v_max_f32_e32 v233, v233, v233
	v_max_f32_e32 v234, v234, v234
	v_max_f32_e32 v235, v235, v235
	v_max_f32_e32 v236, v236, v236
	v_max_f32_e32 v237, v237, v237
	v_max_f32_e32 v238, v238, v238
	v_max_f32_e32 v239, v239, v239
	v_max_f32_e32 v240, v240, v240
	v_max_f32_e32 v241, v241, v241
	v_med3_f32 v226, v226, s62, v95
	v_med3_f32 v227, v227, s62, v95
	v_med3_f32 v228, v228, s62, v95
	v_med3_f32 v229, v229, s62, v95
	v_med3_f32 v230, v230, s62, v95
	v_med3_f32 v231, v231, s62, v95
	v_med3_f32 v232, v232, s62, v95
	v_med3_f32 v233, v233, s62, v95
	v_med3_f32 v234, v234, s62, v95
	v_med3_f32 v235, v235, s62, v95
	v_med3_f32 v236, v236, s62, v95
	v_med3_f32 v237, v237, s62, v95
	v_med3_f32 v238, v238, s62, v95
	v_med3_f32 v239, v239, s62, v95
	v_med3_f32 v240, v240, s62, v95
	v_med3_f32 v241, v241, s62, v95
	v_mov_b32_e32 v242, 0
	v_mov_b32_e32 v243, 0
	v_mov_b32_e32 v244, 0
	v_mov_b32_e32 v245, 0
	v_cvt_pk_fp8_f32 v242, v226, v227
	v_cvt_pk_fp8_f32 v243, v230, v231
	v_cvt_pk_fp8_f32 v244, v234, v235
	v_cvt_pk_fp8_f32 v245, v238, v239
	v_cvt_pk_fp8_f32 v242, v228, v229 op_sel:[0,0,1]
	v_cvt_pk_fp8_f32 v243, v232, v233 op_sel:[0,0,1]
	v_cvt_pk_fp8_f32 v244, v236, v237 op_sel:[0,0,1]
	v_cvt_pk_fp8_f32 v245, v240, v241 op_sel:[0,0,1]
	s_nop 0
	global_store_dwordx4 v80, v[242:245], s[6:7]
	s_waitcnt vmcnt(12)
	v_mul_f32_e32 v144, 0x43000000, v144
	v_mul_f32_e32 v145, 0x43000000, v145
	v_mul_f32_e32 v146, 0x43000000, v146
	v_mul_f32_e32 v147, 0x43000000, v147
	ds_write_b128 v209, v[144:147]
	v_mul_f32_e32 v148, 0x43000000, v148
	v_mul_f32_e32 v149, 0x43000000, v149
	v_mul_f32_e32 v150, 0x43000000, v150
	v_mul_f32_e32 v151, 0x43000000, v151
	ds_write_b128 v209, v[148:151] offset:1024
	v_mul_f32_e32 v152, 0x43000000, v152
	v_mul_f32_e32 v153, 0x43000000, v153
	v_mul_f32_e32 v154, 0x43000000, v154
	v_mul_f32_e32 v155, 0x43000000, v155
	ds_write_b128 v209, v[152:155] offset:2048
	v_mul_f32_e32 v156, 0x43000000, v156
	v_mul_f32_e32 v157, 0x43000000, v157
	v_mul_f32_e32 v158, 0x43000000, v158
	v_mul_f32_e32 v159, 0x43000000, v159
	ds_write_b128 v209, v[156:159] offset:3072
	v_mul_f32_e32 v160, 0x43000000, v160
	v_mul_f32_e32 v161, 0x43000000, v161
	v_mul_f32_e32 v162, 0x43000000, v162
	v_mul_f32_e32 v163, 0x43000000, v163
	ds_write_b128 v209, v[160:163] offset:4096
	v_mul_f32_e32 v164, 0x43000000, v164
	v_mul_f32_e32 v165, 0x43000000, v165
	v_mul_f32_e32 v166, 0x43000000, v166
	v_mul_f32_e32 v167, 0x43000000, v167
	ds_write_b128 v209, v[164:167] offset:5120
	v_mul_f32_e32 v168, 0x43000000, v168
	v_mul_f32_e32 v169, 0x43000000, v169
	v_mul_f32_e32 v170, 0x43000000, v170
	v_mul_f32_e32 v171, 0x43000000, v171
	ds_write_b128 v209, v[168:171] offset:6144
	v_mul_f32_e32 v172, 0x43000000, v172
	v_mul_f32_e32 v173, 0x43000000, v173
	v_mul_f32_e32 v174, 0x43000000, v174
	v_mul_f32_e32 v175, 0x43000000, v175
	ds_write_b128 v209, v[172:175] offset:7168
	s_waitcnt lgkmcnt(0)
	s_barrier
	s_add_u32 s8, s38, 0xc002000
	s_addc_u32 s9, s39, 0
	global_load_dwordx4 v[144:147], v75, s[8:9]
	s_add_u32 s8, s8, 0x8000
	s_addc_u32 s9, s9, 0
	global_load_dwordx4 v[148:151], v75, s[8:9]
	s_add_u32 s8, s8, 0x8000
	s_addc_u32 s9, s9, 0
	global_load_dwordx4 v[152:155], v75, s[8:9]
	s_add_u32 s8, s8, 0x8000
	s_addc_u32 s9, s9, 0
	global_load_dwordx4 v[156:159], v75, s[8:9]
	s_add_u32 s8, s8, 0x8000
	s_addc_u32 s9, s9, 0
	global_load_dwordx4 v[160:163], v75, s[8:9]
	s_add_u32 s8, s8, 0x8000
	s_addc_u32 s9, s9, 0
	global_load_dwordx4 v[164:167], v75, s[8:9]
	s_add_u32 s8, s8, 0x8000
	s_addc_u32 s9, s9, 0
	global_load_dwordx4 v[168:171], v75, s[8:9]
	s_add_u32 s8, s8, 0x8000
	s_addc_u32 s9, s9, 0
	global_load_dwordx4 v[172:175], v75, s[8:9]
	s_add_u32 s6, s40, 0x3000
	s_addc_u32 s7, s41, 0
	ds_read_b32 v226, v211
	ds_read_b32 v227, v211 offset:512
	ds_read_b32 v228, v211 offset:1024
	ds_read_b32 v229, v211 offset:1536
	ds_read_b32 v230, v211 offset:2048
	ds_read_b32 v231, v211 offset:2560
	ds_read_b32 v232, v211 offset:3072
	ds_read_b32 v233, v211 offset:3584
	ds_read_b32 v234, v211 offset:4096
	ds_read_b32 v235, v211 offset:4608
	ds_read_b32 v236, v211 offset:5120
	ds_read_b32 v237, v211 offset:5632
	ds_read_b32 v238, v211 offset:6144
	ds_read_b32 v239, v211 offset:6656
	ds_read_b32 v240, v211 offset:7168
	ds_read_b32 v241, v211 offset:7680
	s_waitcnt lgkmcnt(0)
	v_max_f32_e32 v226, v226, v226
	v_max_f32_e32 v227, v227, v227
	v_max_f32_e32 v228, v228, v228
	v_max_f32_e32 v229, v229, v229
	v_max_f32_e32 v230, v230, v230
	v_max_f32_e32 v231, v231, v231
	v_max_f32_e32 v232, v232, v232
	v_max_f32_e32 v233, v233, v233
	v_max_f32_e32 v234, v234, v234
	v_max_f32_e32 v235, v235, v235
	v_max_f32_e32 v236, v236, v236
	v_max_f32_e32 v237, v237, v237
	v_max_f32_e32 v238, v238, v238
	v_max_f32_e32 v239, v239, v239
	v_max_f32_e32 v240, v240, v240
	v_max_f32_e32 v241, v241, v241
	v_med3_f32 v226, v226, s62, v95
	v_med3_f32 v227, v227, s62, v95
	v_med3_f32 v228, v228, s62, v95
	v_med3_f32 v229, v229, s62, v95
	v_med3_f32 v230, v230, s62, v95
	v_med3_f32 v231, v231, s62, v95
	v_med3_f32 v232, v232, s62, v95
	v_med3_f32 v233, v233, s62, v95
	v_med3_f32 v234, v234, s62, v95
	v_med3_f32 v235, v235, s62, v95
	v_med3_f32 v236, v236, s62, v95
	v_med3_f32 v237, v237, s62, v95
	v_med3_f32 v238, v238, s62, v95
	v_med3_f32 v239, v239, s62, v95
	v_med3_f32 v240, v240, s62, v95
	v_med3_f32 v241, v241, s62, v95
	v_mov_b32_e32 v242, 0
	v_mov_b32_e32 v243, 0
	v_mov_b32_e32 v244, 0
	v_mov_b32_e32 v245, 0
	v_cvt_pk_fp8_f32 v242, v226, v227
	v_cvt_pk_fp8_f32 v243, v230, v231
	v_cvt_pk_fp8_f32 v244, v234, v235
	v_cvt_pk_fp8_f32 v245, v238, v239
	v_cvt_pk_fp8_f32 v242, v228, v229 op_sel:[0,0,1]
	v_cvt_pk_fp8_f32 v243, v232, v233 op_sel:[0,0,1]
	v_cvt_pk_fp8_f32 v244, v236, v237 op_sel:[0,0,1]
	v_cvt_pk_fp8_f32 v245, v240, v241 op_sel:[0,0,1]
	s_nop 0
	global_store_dwordx4 v79, v[242:245], s[6:7]
	ds_read_b32 v226, v213
	ds_read_b32 v227, v213 offset:512
	ds_read_b32 v228, v213 offset:1024
	ds_read_b32 v229, v213 offset:1536
	ds_read_b32 v230, v213 offset:2048
	ds_read_b32 v231, v213 offset:2560
	ds_read_b32 v232, v213 offset:3072
	ds_read_b32 v233, v213 offset:3584
	ds_read_b32 v234, v213 offset:4096
	ds_read_b32 v235, v213 offset:4608
	ds_read_b32 v236, v213 offset:5120
	ds_read_b32 v237, v213 offset:5632
	ds_read_b32 v238, v213 offset:6144
	ds_read_b32 v239, v213 offset:6656
	ds_read_b32 v240, v213 offset:7168
	ds_read_b32 v241, v213 offset:7680
	s_waitcnt lgkmcnt(0)
; #define GAS __attribute__((address_space(1)))
; #define LAS __attribute__((address_space(3)))
; #define LDS_WAIT() asm volatile("s_waitcnt lgkmcnt(0)" ::: "memory")
;     const int pr = item >> 1, kb = 2 * (pr / nblk) + (item & 1), nb = pr % nblk, k0 = 64 * kb, n0 = 32 * nb;
;     const int nr = n0 + (lane & 31); const int sc = MAP == 1 ? src_col_in(nr) : nr;
;     float v[32];
; #pragma unroll
;     for (int i = 0; i < 32; ++i) v[i] = sc >= 0 ? W[(size_t)(k0 + 2 * i + (lane >> 5)) * Nsrc + sc] : 0.f;
; #pragma unroll
;     for (int i = 0; i < 32; ++i) { const int k = k0 + 2 * i + (lane >> 5); float x = v[i] * wscale; if (KS) x *= (k < ksplit ? ksA[k] : ksB[k - ksplit]); scr[(2 * i + (lane >> 5)) * 33 + (lane & 31)] = x; }
;     LDS_WAIT(); asm volatile("" ::: "memory");
;     const int c = lane & 7;
; #pragma unroll
;     for (int j = 0; j < 4; ++j) { const int n = (lane >> 3) + 8 * j; const LAS float* s = scr + (8 * c) * 33 + n;
;         const unsigned long long o = (unsigned long long)pg8::pk4_fp8(s[0 * 33], s[1 * 33], s[2 * 33], s[3 * 33]) | ((unsigned long long)pg8::pk4_fp8(s[4 * 33], s[5 * 33], s[6 * 33], s[7 * 33]) << 32);
;         *(GAS unsigned long long*)(WT + (size_t)(n0 + n) * K + k0 + 8 * c) = o; }
;     LDS_WAIT(); asm volatile("" ::: "memory");
; }
; __global__ void __launch_bounds__(NWAVES * 64, 2) hybrid_fwd(Args args) {
;     ...
;             p0_transpose_item_f8<false>(args.in[16] + (size_t)l * FF * DM, FF, DM, DM / 32, (unsigned char*)(ws + WS_WDN + l * SZ_WDN), 128.f, args.in[16], args.in[16], 0, scr, r, lane);
	v_max_f32_e32 v226, v226, v226
	v_max_f32_e32 v227, v227, v227
	v_max_f32_e32 v228, v228, v228
	v_max_f32_e32 v229, v229, v229
	v_max_f32_e32 v230, v230, v230
	v_max_f32_e32 v231, v231, v231
	v_max_f32_e32 v232, v232, v232
	v_max_f32_e32 v233, v233, v233
	v_max_f32_e32 v234, v234, v234
	v_max_f32_e32 v235, v235, v235
	v_max_f32_e32 v236, v236, v236
	v_max_f32_e32 v237, v237, v237
	v_max_f32_e32 v238, v238, v238
	v_max_f32_e32 v239, v239, v239
	v_max_f32_e32 v240, v240, v240
	v_max_f32_e32 v241, v241, v241
	v_med3_f32 v226, v226, s62, v95
	v_med3_f32 v227, v227, s62, v95
	v_med3_f32 v228, v228, s62, v95
	v_med3_f32 v229, v229, s62, v95
	v_med3_f32 v230, v230, s62, v95
	v_med3_f32 v231, v231, s62, v95
	v_med3_f32 v232, v232, s62, v95
	v_med3_f32 v233, v233, s62, v95
	v_med3_f32 v234, v234, s62, v95
	v_med3_f32 v235, v235, s62, v95
	v_med3_f32 v236, v236, s62, v95
	v_med3_f32 v237, v237, s62, v95
	v_med3_f32 v238, v238, s62, v95
	v_med3_f32 v239, v239, s62, v95
	v_med3_f32 v240, v240, s62, v95
	v_med3_f32 v241, v241, s62, v95
	v_mov_b32_e32 v242, 0
	v_mov_b32_e32 v243, 0
	v_mov_b32_e32 v244, 0
	v_mov_b32_e32 v245, 0
	v_cvt_pk_fp8_f32 v242, v226, v227
	v_cvt_pk_fp8_f32 v243, v230, v231
	v_cvt_pk_fp8_f32 v244, v234, v235
	v_cvt_pk_fp8_f32 v245, v238, v239
	v_cvt_pk_fp8_f32 v242, v228, v229 op_sel:[0,0,1]
	v_cvt_pk_fp8_f32 v243, v232, v233 op_sel:[0,0,1]
	v_cvt_pk_fp8_f32 v244, v236, v237 op_sel:[0,0,1]
	v_cvt_pk_fp8_f32 v245, v240, v241 op_sel:[0,0,1]
	s_nop 0
	global_store_dwordx4 v80, v[242:245], s[6:7]
	s_waitcnt vmcnt(12)
	v_mul_f32_e32 v176, 0x43000000, v176
	v_mul_f32_e32 v177, 0x43000000, v177
	v_mul_f32_e32 v178, 0x43000000, v178
	v_mul_f32_e32 v179, 0x43000000, v179
	ds_write_b128 v210, v[176:179]
	v_mul_f32_e32 v180, 0x43000000, v180
	v_mul_f32_e32 v181, 0x43000000, v181
	v_mul_f32_e32 v182, 0x43000000, v182
	v_mul_f32_e32 v183, 0x43000000, v183
	ds_write_b128 v210, v[180:183] offset:1024
	v_mul_f32_e32 v184, 0x43000000, v184
	v_mul_f32_e32 v185, 0x43000000, v185
	v_mul_f32_e32 v186, 0x43000000, v186
	v_mul_f32_e32 v187, 0x43000000, v187
	ds_write_b128 v210, v[184:187] offset:2048
	v_mul_f32_e32 v188, 0x43000000, v188
	v_mul_f32_e32 v189, 0x43000000, v189
	v_mul_f32_e32 v190, 0x43000000, v190
	v_mul_f32_e32 v191, 0x43000000, v191
	ds_write_b128 v210, v[188:191] offset:3072
	v_mul_f32_e32 v192, 0x43000000, v192
	v_mul_f32_e32 v193, 0x43000000, v193
	v_mul_f32_e32 v194, 0x43000000, v194
	v_mul_f32_e32 v195, 0x43000000, v195
	ds_write_b128 v210, v[192:195] offset:4096
	v_mul_f32_e32 v196, 0x43000000, v196
	v_mul_f32_e32 v197, 0x43000000, v197
	v_mul_f32_e32 v198, 0x43000000, v198
	v_mul_f32_e32 v199, 0x43000000, v199
	ds_write_b128 v210, v[196:199] offset:5120
	v_mul_f32_e32 v200, 0x43000000, v200
	v_mul_f32_e32 v201, 0x43000000, v201
	v_mul_f32_e32 v202, 0x43000000, v202
	v_mul_f32_e32 v203, 0x43000000, v203
	ds_write_b128 v210, v[200:203] offset:6144
	v_mul_f32_e32 v204, 0x43000000, v204
	v_mul_f32_e32 v205, 0x43000000, v205
	v_mul_f32_e32 v206, 0x43000000, v206
	v_mul_f32_e32 v207, 0x43000000, v207
	ds_write_b128 v210, v[204:207] offset:7168
	s_waitcnt lgkmcnt(0)
	s_barrier
	s_add_u32 s8, s38, 0xc003000
	s_addc_u32 s9, s39, 0
	global_load_dwordx4 v[176:179], v75, s[8:9]
	s_add_u32 s8, s8, 0x8000
	s_addc_u32 s9, s9, 0
	global_load_dwordx4 v[180:183], v75, s[8:9]
	s_add_u32 s8, s8, 0x8000
	s_addc_u32 s9, s9, 0
	global_load_dwordx4 v[184:187], v75, s[8:9]
	s_add_u32 s8, s8, 0x8000
	s_addc_u32 s9, s9, 0
	global_load_dwordx4 v[188:191], v75, s[8:9]
	s_add_u32 s8, s8, 0x8000
	s_addc_u32 s9, s9, 0
	global_load_dwordx4 v[192:195], v75, s[8:9]
	s_add_u32 s8, s8, 0x8000
	s_addc_u32 s9, s9, 0
	global_load_dwordx4 v[196:199], v75, s[8:9]
	s_add_u32 s8, s8, 0x8000
	s_addc_u32 s9, s9, 0
	global_load_dwordx4 v[200:203], v75, s[8:9]
	s_add_u32 s8, s8, 0x8000
	s_addc_u32 s9, s9, 0
	global_load_dwordx4 v[204:207], v75, s[8:9]
	s_add_u32 s6, s40, 0x1003000
	s_addc_u32 s7, s41, 0
	ds_read_b32 v226, v212
	ds_read_b32 v227, v212 offset:512
	ds_read_b32 v228, v212 offset:1024
	ds_read_b32 v229, v212 offset:1536
	ds_read_b32 v230, v212 offset:2048
	ds_read_b32 v231, v212 offset:2560
	ds_read_b32 v232, v212 offset:3072
	ds_read_b32 v233, v212 offset:3584
	ds_read_b32 v234, v212 offset:4096
	ds_read_b32 v235, v212 offset:4608
	ds_read_b32 v236, v212 offset:5120
	ds_read_b32 v237, v212 offset:5632
	ds_read_b32 v238, v212 offset:6144
	ds_read_b32 v239, v212 offset:6656
	ds_read_b32 v240, v212 offset:7168
	ds_read_b32 v241, v212 offset:7680
	s_waitcnt lgkmcnt(0)
	v_max_f32_e32 v226, v226, v226
	v_max_f32_e32 v227, v227, v227
	v_max_f32_e32 v228, v228, v228
	v_max_f32_e32 v229, v229, v229
	v_max_f32_e32 v230, v230, v230
	v_max_f32_e32 v231, v231, v231
	v_max_f32_e32 v232, v232, v232
	v_max_f32_e32 v233, v233, v233
	v_max_f32_e32 v234, v234, v234
	v_max_f32_e32 v235, v235, v235
	v_max_f32_e32 v236, v236, v236
	v_max_f32_e32 v237, v237, v237
	v_max_f32_e32 v238, v238, v238
	v_max_f32_e32 v239, v239, v239
	v_max_f32_e32 v240, v240, v240
	v_max_f32_e32 v241, v241, v241
	v_med3_f32 v226, v226, s62, v95
	v_med3_f32 v227, v227, s62, v95
	v_med3_f32 v228, v228, s62, v95
	v_med3_f32 v229, v229, s62, v95
	v_med3_f32 v230, v230, s62, v95
	v_med3_f32 v231, v231, s62, v95
	v_med3_f32 v232, v232, s62, v95
	v_med3_f32 v233, v233, s62, v95
	v_med3_f32 v234, v234, s62, v95
	v_med3_f32 v235, v235, s62, v95
	v_med3_f32 v236, v236, s62, v95
	v_med3_f32 v237, v237, s62, v95
	v_med3_f32 v238, v238, s62, v95
	v_med3_f32 v239, v239, s62, v95
	v_med3_f32 v240, v240, s62, v95
	v_med3_f32 v241, v241, s62, v95
	v_mov_b32_e32 v242, 0
	v_mov_b32_e32 v243, 0
	v_mov_b32_e32 v244, 0
	v_mov_b32_e32 v245, 0
	v_cvt_pk_fp8_f32 v242, v226, v227
	v_cvt_pk_fp8_f32 v243, v230, v231
	v_cvt_pk_fp8_f32 v244, v234, v235
	v_cvt_pk_fp8_f32 v245, v238, v239
	v_cvt_pk_fp8_f32 v242, v228, v229 op_sel:[0,0,1]
	v_cvt_pk_fp8_f32 v243, v232, v233 op_sel:[0,0,1]
	v_cvt_pk_fp8_f32 v244, v236, v237 op_sel:[0,0,1]
	v_cvt_pk_fp8_f32 v245, v240, v241 op_sel:[0,0,1]
	s_nop 0
	global_store_dwordx4 v79, v[242:245], s[6:7]
	ds_read_b32 v226, v214
	ds_read_b32 v227, v214 offset:512
	ds_read_b32 v228, v214 offset:1024
	ds_read_b32 v229, v214 offset:1536
	ds_read_b32 v230, v214 offset:2048
	ds_read_b32 v231, v214 offset:2560
	ds_read_b32 v232, v214 offset:3072
	ds_read_b32 v233, v214 offset:3584
	ds_read_b32 v234, v214 offset:4096
	ds_read_b32 v235, v214 offset:4608
	ds_read_b32 v236, v214 offset:5120
	ds_read_b32 v237, v214 offset:5632
	ds_read_b32 v238, v214 offset:6144
	ds_read_b32 v239, v214 offset:6656
	ds_read_b32 v240, v214 offset:7168
	ds_read_b32 v241, v214 offset:7680
	s_waitcnt lgkmcnt(0)
; #define GAS __attribute__((address_space(1)))
; #define LAS __attribute__((address_space(3)))
; #define LDS_WAIT() asm volatile("s_waitcnt lgkmcnt(0)" ::: "memory")
; __device__ __forceinline__ int src_col_in(int c) {
;     if (c < 5120) { const int blk = c >> 7, p = c & 127; const bool rope = blk < 16 || ((((blk - 16) >> 2) & 1) == 0); const int d = rope ? (p >> 1) + 64 * (p & 1) : p; return blk * 128 + d; }
;     if (c < OFF_Z) return c + 2096;
;     if (c < OFF_G) return c - 4048;
;     if (c < OFF_DT) return 5120 + (c - OFF_G);
;     if (c < NSRC) return c;
;     return -1;
; }
;     const int pr = item >> 1, kb = 2 * (pr / nblk) + (item & 1), nb = pr % nblk, k0 = 64 * kb, n0 = 32 * nb;
;     const int nr = n0 + (lane & 31); const int sc = MAP == 1 ? src_col_in(nr) : nr;
;     float v[32];
; #pragma unroll
;     for (int i = 0; i < 32; ++i) v[i] = sc >= 0 ? W[(size_t)(k0 + 2 * i + (lane >> 5)) * Nsrc + sc] : 0.f;
; #pragma unroll
;     for (int i = 0; i < 32; ++i) { const int k = k0 + 2 * i + (lane >> 5); float x = v[i] * wscale; if (KS) x *= (k < ksplit ? ksA[k] : ksB[k - ksplit]); scr[(2 * i + (lane >> 5)) * 33 + (lane & 31)] = x; }
;     LDS_WAIT(); asm volatile("" ::: "memory");
;     const int c = lane & 7;
; #pragma unroll
;     for (int j = 0; j < 4; ++j) { const int n = (lane >> 3) + 8 * j; const LAS float* s = scr + (8 * c) * 33 + n;
;         const unsigned long long o = (unsigned long long)pg8::pk4_fp8(s[0 * 33], s[1 * 33], s[2 * 33], s[3 * 33]) | ((unsigned long long)pg8::pk4_fp8(s[4 * 33], s[5 * 33], s[6 * 33], s[7 * 33]) << 32);
;         *(GAS unsigned long long*)(WT + (size_t)(n0 + n) * K + k0 + 8 * c) = o; }
;     LDS_WAIT(); asm volatile("" ::: "memory");
; }
	v_max_f32_e32 v226, v226, v226
	v_max_f32_e32 v227, v227, v227
	v_max_f32_e32 v228, v228, v228
	v_max_f32_e32 v229, v229, v229
	v_max_f32_e32 v230, v230, v230
	v_max_f32_e32 v231, v231, v231
	v_max_f32_e32 v232, v232, v232
	v_max_f32_e32 v233, v233, v233
	v_max_f32_e32 v234, v234, v234
	v_max_f32_e32 v235, v235, v235
	v_max_f32_e32 v236, v236, v236
	v_max_f32_e32 v237, v237, v237
	v_max_f32_e32 v238, v238, v238
	v_max_f32_e32 v239, v239, v239
	v_max_f32_e32 v240, v240, v240
	v_max_f32_e32 v241, v241, v241
	v_med3_f32 v226, v226, s62, v95
	v_med3_f32 v227, v227, s62, v95
	v_med3_f32 v228, v228, s62, v95
	v_med3_f32 v229, v229, s62, v95
	v_med3_f32 v230, v230, s62, v95
	v_med3_f32 v231, v231, s62, v95
	v_med3_f32 v232, v232, s62, v95
	v_med3_f32 v233, v233, s62, v95
	v_med3_f32 v234, v234, s62, v95
	v_med3_f32 v235, v235, s62, v95
	v_med3_f32 v236, v236, s62, v95
	v_med3_f32 v237, v237, s62, v95
	v_med3_f32 v238, v238, s62, v95
	v_med3_f32 v239, v239, s62, v95
	v_med3_f32 v240, v240, s62, v95
	v_med3_f32 v241, v241, s62, v95
	v_mov_b32_e32 v242, 0
	v_mov_b32_e32 v243, 0
	v_mov_b32_e32 v244, 0
	v_mov_b32_e32 v245, 0
	v_cvt_pk_fp8_f32 v242, v226, v227
	v_cvt_pk_fp8_f32 v243, v230, v231
	v_cvt_pk_fp8_f32 v244, v234, v235
	v_cvt_pk_fp8_f32 v245, v238, v239
	v_cvt_pk_fp8_f32 v242, v228, v229 op_sel:[0,0,1]
	v_cvt_pk_fp8_f32 v243, v232, v233 op_sel:[0,0,1]
	v_cvt_pk_fp8_f32 v244, v236, v237 op_sel:[0,0,1]
	v_cvt_pk_fp8_f32 v245, v240, v241 op_sel:[0,0,1]
	s_nop 0
	global_store_dwordx4 v80, v[242:245], s[6:7]
	s_waitcnt vmcnt(12)
	v_mul_f32_e32 v144, 0x43000000, v144
	v_mul_f32_e32 v145, 0x43000000, v145
	v_mul_f32_e32 v146, 0x43000000, v146
	v_mul_f32_e32 v147, 0x43000000, v147
	ds_write_b128 v209, v[144:147]
	v_mul_f32_e32 v148, 0x43000000, v148
	v_mul_f32_e32 v149, 0x43000000, v149
	v_mul_f32_e32 v150, 0x43000000, v150
	v_mul_f32_e32 v151, 0x43000000, v151
	ds_write_b128 v209, v[148:151] offset:1024
	v_mul_f32_e32 v152, 0x43000000, v152
	v_mul_f32_e32 v153, 0x43000000, v153
	v_mul_f32_e32 v154, 0x43000000, v154
	v_mul_f32_e32 v155, 0x43000000, v155
	ds_write_b128 v209, v[152:155] offset:2048
	v_mul_f32_e32 v156, 0x43000000, v156
	v_mul_f32_e32 v157, 0x43000000, v157
	v_mul_f32_e32 v158, 0x43000000, v158
	v_mul_f32_e32 v159, 0x43000000, v159
	ds_write_b128 v209, v[156:159] offset:3072
	v_mul_f32_e32 v160, 0x43000000, v160
	v_mul_f32_e32 v161, 0x43000000, v161
	v_mul_f32_e32 v162, 0x43000000, v162
	v_mul_f32_e32 v163, 0x43000000, v163
	ds_write_b128 v209, v[160:163] offset:4096
	v_mul_f32_e32 v164, 0x43000000, v164
	v_mul_f32_e32 v165, 0x43000000, v165
	v_mul_f32_e32 v166, 0x43000000, v166
	v_mul_f32_e32 v167, 0x43000000, v167
	ds_write_b128 v209, v[164:167] offset:5120
	v_mul_f32_e32 v168, 0x43000000, v168
	v_mul_f32_e32 v169, 0x43000000, v169
	v_mul_f32_e32 v170, 0x43000000, v170
	v_mul_f32_e32 v171, 0x43000000, v171
	ds_write_b128 v209, v[168:171] offset:6144
	v_mul_f32_e32 v172, 0x43000000, v172
	v_mul_f32_e32 v173, 0x43000000, v173
	v_mul_f32_e32 v174, 0x43000000, v174
	v_mul_f32_e32 v175, 0x43000000, v175
	ds_write_b128 v209, v[172:175] offset:7168
	s_waitcnt lgkmcnt(0)
	s_barrier
	s_add_i32 s24, s23, 0
	s_lshl_b32 s20, s24, 7
	s_cmp_lt_u32 s24, 40
	s_cselect_b32 s21, 0, 0x830
	s_cmp_lt_u32 s24, 72
	s_cselect_b32 s21, s21, 0xfffff030
	s_add_i32 s20, s20, s21
	s_lshl_b32 s20, s20, 2
	s_add_u32 s8, s46, s20
	s_addc_u32 s9, s47, 0
	global_load_dwordx4 v[144:147], v76, s[8:9]
	s_add_u32 s8, s8, 0x16280
	s_addc_u32 s9, s9, 0
	global_load_dwordx4 v[148:151], v76, s[8:9]
	s_add_u32 s8, s8, 0x16280
	s_addc_u32 s9, s9, 0
	global_load_dwordx4 v[152:155], v76, s[8:9]
	s_add_u32 s8, s8, 0x16280
	s_addc_u32 s9, s9, 0
	global_load_dwordx4 v[156:159], v76, s[8:9]
	s_add_u32 s8, s8, 0x16280
	s_addc_u32 s9, s9, 0
	global_load_dwordx4 v[160:163], v76, s[8:9]
	s_add_u32 s8, s8, 0x16280
	s_addc_u32 s9, s9, 0
	global_load_dwordx4 v[164:167], v76, s[8:9]
	s_add_u32 s8, s8, 0x16280
	s_addc_u32 s9, s9, 0
	global_load_dwordx4 v[168:171], v76, s[8:9]
	s_add_u32 s8, s8, 0x16280
	s_addc_u32 s9, s9, 0
	global_load_dwordx4 v[172:175], v76, s[8:9]
	s_add_u32 s6, s40, 0x2003000
	s_addc_u32 s7, s41, 0
	ds_read_b32 v226, v211
	ds_read_b32 v227, v211 offset:512
	ds_read_b32 v228, v211 offset:1024
	ds_read_b32 v229, v211 offset:1536
	ds_read_b32 v230, v211 offset:2048
	ds_read_b32 v231, v211 offset:2560
	ds_read_b32 v232, v211 offset:3072
	ds_read_b32 v233, v211 offset:3584
	ds_read_b32 v234, v211 offset:4096
	ds_read_b32 v235, v211 offset:4608
	ds_read_b32 v236, v211 offset:5120
	ds_read_b32 v237, v211 offset:5632
	ds_read_b32 v238, v211 offset:6144
	ds_read_b32 v239, v211 offset:6656
	ds_read_b32 v240, v211 offset:7168
	ds_read_b32 v241, v211 offset:7680
	s_waitcnt lgkmcnt(0)
; #define GAS __attribute__((address_space(1)))
; #define LAS __attribute__((address_space(3)))
; #define LDS_WAIT() asm volatile("s_waitcnt lgkmcnt(0)" ::: "memory")
;     const int pr = item >> 1, kb = 2 * (pr / nblk) + (item & 1), nb = pr % nblk, k0 = 64 * kb, n0 = 32 * nb;
;     const int nr = n0 + (lane & 31); const int sc = MAP == 1 ? src_col_in(nr) : nr;
;     float v[32];
; #pragma unroll
;     for (int i = 0; i < 32; ++i) v[i] = sc >= 0 ? W[(size_t)(k0 + 2 * i + (lane >> 5)) * Nsrc + sc] : 0.f;
; #pragma unroll
;     for (int i = 0; i < 32; ++i) { const int k = k0 + 2 * i + (lane >> 5); float x = v[i] * wscale; if (KS) x *= (k < ksplit ? ksA[k] : ksB[k - ksplit]); scr[(2 * i + (lane >> 5)) * 33 + (lane & 31)] = x; }
;     LDS_WAIT(); asm volatile("" ::: "memory");
;     const int c = lane & 7;
; #pragma unroll
;     for (int j = 0; j < 4; ++j) { const int n = (lane >> 3) + 8 * j; const LAS float* s = scr + (8 * c) * 33 + n;
;         const unsigned long long o = (unsigned long long)pg8::pk4_fp8(s[0 * 33], s[1 * 33], s[2 * 33], s[3 * 33]) | ((unsigned long long)pg8::pk4_fp8(s[4 * 33], s[5 * 33], s[6 * 33], s[7 * 33]) << 32);
;         *(GAS unsigned long long*)(WT + (size_t)(n0 + n) * K + k0 + 8 * c) = o; }
;     LDS_WAIT(); asm volatile("" ::: "memory");
; }
	v_max_f32_e32 v226, v226, v226
	v_max_f32_e32 v227, v227, v227
	v_max_f32_e32 v228, v228, v228
	v_max_f32_e32 v229, v229, v229
	v_max_f32_e32 v230, v230, v230
	v_max_f32_e32 v231, v231, v231
	v_max_f32_e32 v232, v232, v232
	v_max_f32_e32 v233, v233, v233
	v_max_f32_e32 v234, v234, v234
	v_max_f32_e32 v235, v235, v235
	v_max_f32_e32 v236, v236, v236
	v_max_f32_e32 v237, v237, v237
	v_max_f32_e32 v238, v238, v238
	v_max_f32_e32 v239, v239, v239
	v_max_f32_e32 v240, v240, v240
	v_max_f32_e32 v241, v241, v241
	v_med3_f32 v226, v226, s62, v95
	v_med3_f32 v227, v227, s62, v95
	v_med3_f32 v228, v228, s62, v95
	v_med3_f32 v229, v229, s62, v95
	v_med3_f32 v230, v230, s62, v95
	v_med3_f32 v231, v231, s62, v95
	v_med3_f32 v232, v232, s62, v95
	v_med3_f32 v233, v233, s62, v95
	v_med3_f32 v234, v234, s62, v95
	v_med3_f32 v235, v235, s62, v95
	v_med3_f32 v236, v236, s62, v95
	v_med3_f32 v237, v237, s62, v95
	v_med3_f32 v238, v238, s62, v95
	v_med3_f32 v239, v239, s62, v95
	v_med3_f32 v240, v240, s62, v95
	v_med3_f32 v241, v241, s62, v95
	v_mov_b32_e32 v242, 0
	v_mov_b32_e32 v243, 0
	v_mov_b32_e32 v244, 0
	v_mov_b32_e32 v245, 0
	v_cvt_pk_fp8_f32 v242, v226, v227
	v_cvt_pk_fp8_f32 v243, v230, v231
	v_cvt_pk_fp8_f32 v244, v234, v235
	v_cvt_pk_fp8_f32 v245, v238, v239
	v_cvt_pk_fp8_f32 v242, v228, v229 op_sel:[0,0,1]
	v_cvt_pk_fp8_f32 v243, v232, v233 op_sel:[0,0,1]
	v_cvt_pk_fp8_f32 v244, v236, v237 op_sel:[0,0,1]
	v_cvt_pk_fp8_f32 v245, v240, v241 op_sel:[0,0,1]
	s_nop 0
	global_store_dwordx4 v79, v[242:245], s[6:7]
	ds_read_b32 v226, v213
	ds_read_b32 v227, v213 offset:512
	ds_read_b32 v228, v213 offset:1024
	ds_read_b32 v229, v213 offset:1536
	ds_read_b32 v230, v213 offset:2048
	ds_read_b32 v231, v213 offset:2560
	ds_read_b32 v232, v213 offset:3072
	ds_read_b32 v233, v213 offset:3584
	ds_read_b32 v234, v213 offset:4096
	ds_read_b32 v235, v213 offset:4608
	ds_read_b32 v236, v213 offset:5120
	ds_read_b32 v237, v213 offset:5632
	ds_read_b32 v238, v213 offset:6144
	ds_read_b32 v239, v213 offset:6656
	ds_read_b32 v240, v213 offset:7168
	ds_read_b32 v241, v213 offset:7680
	s_waitcnt lgkmcnt(0)
	v_max_f32_e32 v226, v226, v226
	v_max_f32_e32 v227, v227, v227
	v_max_f32_e32 v228, v228, v228
	v_max_f32_e32 v229, v229, v229
	v_max_f32_e32 v230, v230, v230
	v_max_f32_e32 v231, v231, v231
	v_max_f32_e32 v232, v232, v232
	v_max_f32_e32 v233, v233, v233
	v_max_f32_e32 v234, v234, v234
	v_max_f32_e32 v235, v235, v235
	v_max_f32_e32 v236, v236, v236
	v_max_f32_e32 v237, v237, v237
	v_max_f32_e32 v238, v238, v238
	v_max_f32_e32 v239, v239, v239
	v_max_f32_e32 v240, v240, v240
	v_max_f32_e32 v241, v241, v241
	v_med3_f32 v226, v226, s62, v95
	v_med3_f32 v227, v227, s62, v95
	v_med3_f32 v228, v228, s62, v95
	v_med3_f32 v229, v229, s62, v95
	v_med3_f32 v230, v230, s62, v95
	v_med3_f32 v231, v231, s62, v95
	v_med3_f32 v232, v232, s62, v95
	v_med3_f32 v233, v233, s62, v95
	v_med3_f32 v234, v234, s62, v95
	v_med3_f32 v235, v235, s62, v95
	v_med3_f32 v236, v236, s62, v95
	v_med3_f32 v237, v237, s62, v95
	v_med3_f32 v238, v238, s62, v95
	v_med3_f32 v239, v239, s62, v95
	v_med3_f32 v240, v240, s62, v95
	v_med3_f32 v241, v241, s62, v95
	v_mov_b32_e32 v242, 0
	v_mov_b32_e32 v243, 0
	v_mov_b32_e32 v244, 0
	v_mov_b32_e32 v245, 0
	v_cvt_pk_fp8_f32 v242, v226, v227
	v_cvt_pk_fp8_f32 v243, v230, v231
	v_cvt_pk_fp8_f32 v244, v234, v235
	v_cvt_pk_fp8_f32 v245, v238, v239
	v_cvt_pk_fp8_f32 v242, v228, v229 op_sel:[0,0,1]
	v_cvt_pk_fp8_f32 v243, v232, v233 op_sel:[0,0,1]
	v_cvt_pk_fp8_f32 v244, v236, v237 op_sel:[0,0,1]
	v_cvt_pk_fp8_f32 v245, v240, v241 op_sel:[0,0,1]
	s_nop 0
	global_store_dwordx4 v80, v[242:245], s[6:7]
	s_waitcnt vmcnt(12)
	v_mul_f32_e32 v176, 0x43000000, v176
	v_mul_f32_e32 v177, 0x43000000, v177
	v_mul_f32_e32 v178, 0x43000000, v178
	v_mul_f32_e32 v179, 0x43000000, v179
	ds_write_b128 v210, v[176:179]
	v_mul_f32_e32 v180, 0x43000000, v180
	v_mul_f32_e32 v181, 0x43000000, v181
	v_mul_f32_e32 v182, 0x43000000, v182
	v_mul_f32_e32 v183, 0x43000000, v183
	ds_write_b128 v210, v[180:183] offset:1024
	v_mul_f32_e32 v184, 0x43000000, v184
	v_mul_f32_e32 v185, 0x43000000, v185
	v_mul_f32_e32 v186, 0x43000000, v186
	v_mul_f32_e32 v187, 0x43000000, v187
	ds_write_b128 v210, v[184:187] offset:2048
	v_mul_f32_e32 v188, 0x43000000, v188
	v_mul_f32_e32 v189, 0x43000000, v189
	v_mul_f32_e32 v190, 0x43000000, v190
	v_mul_f32_e32 v191, 0x43000000, v191
	ds_write_b128 v210, v[188:191] offset:3072
	v_mul_f32_e32 v192, 0x43000000, v192
	v_mul_f32_e32 v193, 0x43000000, v193
	v_mul_f32_e32 v194, 0x43000000, v194
	v_mul_f32_e32 v195, 0x43000000, v195
	ds_write_b128 v210, v[192:195] offset:4096
	v_mul_f32_e32 v196, 0x43000000, v196
	v_mul_f32_e32 v197, 0x43000000, v197
	v_mul_f32_e32 v198, 0x43000000, v198
	v_mul_f32_e32 v199, 0x43000000, v199
	ds_write_b128 v210, v[196:199] offset:5120
	v_mul_f32_e32 v200, 0x43000000, v200
	v_mul_f32_e32 v201, 0x43000000, v201
	v_mul_f32_e32 v202, 0x43000000, v202
	v_mul_f32_e32 v203, 0x43000000, v203
	ds_write_b128 v210, v[200:203] offset:6144
	v_mul_f32_e32 v204, 0x43000000, v204
	v_mul_f32_e32 v205, 0x43000000, v205
	v_mul_f32_e32 v206, 0x43000000, v206
	v_mul_f32_e32 v207, 0x43000000, v207
	ds_write_b128 v210, v[204:207] offset:7168
	s_waitcnt lgkmcnt(0)
	s_barrier
; template <int MAP, bool KS, bool KPERM = false>
; __device__ __forceinline__ void p0_transpose_item(const float* W, int K, int Nsrc, int nblk, bf16* WT, const float* ksA, const float* ksB, int ksplit, LAS float* scr, int item, int lane) {
;     const int kb = item / nblk, nb = item % nblk, k0 = 64 * kb, n0 = 32 * nb;
;     const int nr = n0 + (lane & 31); const int sc = MAP == 1 ? src_col_in(nr) : (MAP == 2 ? nat_dim(nr) : nr);
;     float v[32];
; #pragma unroll
;     for (int i = 0; i < 32; ++i) { const int k = k0 + 2 * i + (lane >> 5); const int ksrc = KPERM ? ((k & ~127) + nat_dim(k & 127)) : k;
;         v[i] = sc >= 0 ? W[(size_t)ksrc * Nsrc + sc] : 0.f; }
; #pragma unroll
;     for (int i = 0; i < 32; ++i) { const int kk = 2 * i + (lane >> 5); const int k = k0 + kk;
;         if (KS) v[i] *= (k < ksplit ? ksA[k] : ksB[k - ksplit]);
;         scr[kk * 33 + (lane & 31)] = v[i]; }
;     LDS_WAIT(); asm volatile("" ::: "memory");
;     const int c = lane & 7;
; #pragma unroll
;     for (int j = 0; j < 4; ++j) { const int n = (lane >> 3) + 8 * j; const LAS float* s = scr + (8 * c) * 33 + n;
;         v4u o; o.x = pk2(s[0 * 33], s[1 * 33]); o.y = pk2(s[2 * 33], s[3 * 33]); o.z = pk2(s[4 * 33], s[5 * 33]); o.w = pk2(s[6 * 33], s[7 * 33]);
;         *(GAS v4u*)(WT + (size_t)(n0 + n) * K + k0 + 8 * c) = o; }
;     LDS_WAIT(); asm volatile("" ::: "memory");
; }
;     const int pr = item >> 1, kb = 2 * (pr / nblk) + (item & 1), nb = pr % nblk, k0 = 64 * kb, n0 = 32 * nb;
;     const int nr = n0 + (lane & 31); const int sc = MAP == 1 ? src_col_in(nr) : nr;
;     float v[32];
; #pragma unroll
;     for (int i = 0; i < 32; ++i) v[i] = sc >= 0 ? W[(size_t)(k0 + 2 * i + (lane >> 5)) * Nsrc + sc] : 0.f;
; #pragma unroll
;     for (int i = 0; i < 32; ++i) { const int k = k0 + 2 * i + (lane >> 5); float x = v[i] * wscale; if (KS) x *= (k < ksplit ? ksA[k] : ksB[k - ksplit]); scr[(2 * i + (lane >> 5)) * 33 + (lane & 31)] = x; }
;     LDS_WAIT(); asm volatile("" ::: "memory");
;     const int c = lane & 7;
; #pragma unroll
;     for (int j = 0; j < 4; ++j) { const int n = (lane >> 3) + 8 * j; const LAS float* s = scr + (8 * c) * 33 + n;
;         const unsigned long long o = (unsigned long long)pg8::pk4_fp8(s[0 * 33], s[1 * 33], s[2 * 33], s[3 * 33]) | ((unsigned long long)pg8::pk4_fp8(s[4 * 33], s[5 * 33], s[6 * 33], s[7 * 33]) << 32);
	s_add_i32 s24, s23, 8
	s_lshl_b32 s20, s24, 7
	s_cmp_lt_u32 s24, 40
	s_cselect_b32 s21, 0, 0x830
	s_cmp_lt_u32 s24, 72
	s_cselect_b32 s21, s21, 0xfffff030
	s_add_i32 s20, s20, s21
	s_lshl_b32 s20, s20, 2
	s_add_u32 s8, s46, s20
	s_addc_u32 s9, s47, 0
	global_load_dwordx4 v[176:179], v76, s[8:9]
	s_add_u32 s8, s8, 0x16280
	s_addc_u32 s9, s9, 0
	global_load_dwordx4 v[180:183], v76, s[8:9]
	s_add_u32 s8, s8, 0x16280
	s_addc_u32 s9, s9, 0
	global_load_dwordx4 v[184:187], v76, s[8:9]
	s_add_u32 s8, s8, 0x16280
	s_addc_u32 s9, s9, 0
	global_load_dwordx4 v[188:191], v76, s[8:9]
	s_add_u32 s8, s8, 0x16280
	s_addc_u32 s9, s9, 0
	global_load_dwordx4 v[192:195], v76, s[8:9]
	s_add_u32 s8, s8, 0x16280
	s_addc_u32 s9, s9, 0
	global_load_dwordx4 v[196:199], v76, s[8:9]
	s_add_u32 s8, s8, 0x16280
	s_addc_u32 s9, s9, 0
	global_load_dwordx4 v[200:203], v76, s[8:9]
	s_add_u32 s8, s8, 0x16280
	s_addc_u32 s9, s9, 0
	global_load_dwordx4 v[204:207], v76, s[8:9]
	s_add_u32 s6, s40, 0x3003000
	s_addc_u32 s7, s41, 0
	ds_read_b32 v226, v212
	ds_read_b32 v227, v212 offset:512
	ds_read_b32 v228, v212 offset:1024
	ds_read_b32 v229, v212 offset:1536
	ds_read_b32 v230, v212 offset:2048
	ds_read_b32 v231, v212 offset:2560
	ds_read_b32 v232, v212 offset:3072
	ds_read_b32 v233, v212 offset:3584
	ds_read_b32 v234, v212 offset:4096
	ds_read_b32 v235, v212 offset:4608
	ds_read_b32 v236, v212 offset:5120
	ds_read_b32 v237, v212 offset:5632
	ds_read_b32 v238, v212 offset:6144
	ds_read_b32 v239, v212 offset:6656
	ds_read_b32 v240, v212 offset:7168
	ds_read_b32 v241, v212 offset:7680
	s_waitcnt lgkmcnt(0)
	v_max_f32_e32 v226, v226, v226
	v_max_f32_e32 v227, v227, v227
	v_max_f32_e32 v228, v228, v228
	v_max_f32_e32 v229, v229, v229
	v_max_f32_e32 v230, v230, v230
	v_max_f32_e32 v231, v231, v231
	v_max_f32_e32 v232, v232, v232
	v_max_f32_e32 v233, v233, v233
	v_max_f32_e32 v234, v234, v234
	v_max_f32_e32 v235, v235, v235
	v_max_f32_e32 v236, v236, v236
	v_max_f32_e32 v237, v237, v237
	v_max_f32_e32 v238, v238, v238
	v_max_f32_e32 v239, v239, v239
	v_max_f32_e32 v240, v240, v240
	v_max_f32_e32 v241, v241, v241
	v_med3_f32 v226, v226, s62, v95
	v_med3_f32 v227, v227, s62, v95
	v_med3_f32 v228, v228, s62, v95
	v_med3_f32 v229, v229, s62, v95
	v_med3_f32 v230, v230, s62, v95
	v_med3_f32 v231, v231, s62, v95
	v_med3_f32 v232, v232, s62, v95
	v_med3_f32 v233, v233, s62, v95
	v_med3_f32 v234, v234, s62, v95
	v_med3_f32 v235, v235, s62, v95
	v_med3_f32 v236, v236, s62, v95
	v_med3_f32 v237, v237, s62, v95
	v_med3_f32 v238, v238, s62, v95
	v_med3_f32 v239, v239, s62, v95
	v_med3_f32 v240, v240, s62, v95
	v_med3_f32 v241, v241, s62, v95
	v_mov_b32_e32 v242, 0
	v_mov_b32_e32 v243, 0
	v_mov_b32_e32 v244, 0
	v_mov_b32_e32 v245, 0
	v_cvt_pk_fp8_f32 v242, v226, v227
	v_cvt_pk_fp8_f32 v243, v230, v231
	v_cvt_pk_fp8_f32 v244, v234, v235
	v_cvt_pk_fp8_f32 v245, v238, v239
	v_cvt_pk_fp8_f32 v242, v228, v229 op_sel:[0,0,1]
	v_cvt_pk_fp8_f32 v243, v232, v233 op_sel:[0,0,1]
	v_cvt_pk_fp8_f32 v244, v236, v237 op_sel:[0,0,1]
	v_cvt_pk_fp8_f32 v245, v240, v241 op_sel:[0,0,1]
	s_nop 0
	global_store_dwordx4 v79, v[242:245], s[6:7]
	ds_read_b32 v226, v214
	ds_read_b32 v227, v214 offset:512
	ds_read_b32 v228, v214 offset:1024
	ds_read_b32 v229, v214 offset:1536
	ds_read_b32 v230, v214 offset:2048
	ds_read_b32 v231, v214 offset:2560
	ds_read_b32 v232, v214 offset:3072
	ds_read_b32 v233, v214 offset:3584
	ds_read_b32 v234, v214 offset:4096
	ds_read_b32 v235, v214 offset:4608
	ds_read_b32 v236, v214 offset:5120
	ds_read_b32 v237, v214 offset:5632
	ds_read_b32 v238, v214 offset:6144
	ds_read_b32 v239, v214 offset:6656
	ds_read_b32 v240, v214 offset:7168
	ds_read_b32 v241, v214 offset:7680
	s_waitcnt lgkmcnt(0)
	v_max_f32_e32 v226, v226, v226
	v_max_f32_e32 v227, v227, v227
	v_max_f32_e32 v228, v228, v228
	v_max_f32_e32 v229, v229, v229
	v_max_f32_e32 v230, v230, v230
	v_max_f32_e32 v231, v231, v231
	v_max_f32_e32 v232, v232, v232
	v_max_f32_e32 v233, v233, v233
	v_max_f32_e32 v234, v234, v234
	v_max_f32_e32 v235, v235, v235
	v_max_f32_e32 v236, v236, v236
	v_max_f32_e32 v237, v237, v237
	v_max_f32_e32 v238, v238, v238
	v_max_f32_e32 v239, v239, v239
	v_max_f32_e32 v240, v240, v240
	v_max_f32_e32 v241, v241, v241
	v_med3_f32 v226, v226, s62, v95
	v_med3_f32 v227, v227, s62, v95
	v_med3_f32 v228, v228, s62, v95
	v_med3_f32 v229, v229, s62, v95
	v_med3_f32 v230, v230, s62, v95
	v_med3_f32 v231, v231, s62, v95
	v_med3_f32 v232, v232, s62, v95
	v_med3_f32 v233, v233, s62, v95
	v_med3_f32 v234, v234, s62, v95
	v_med3_f32 v235, v235, s62, v95
	v_med3_f32 v236, v236, s62, v95
	v_med3_f32 v237, v237, s62, v95
	v_med3_f32 v238, v238, s62, v95
	v_med3_f32 v239, v239, s62, v95
	v_med3_f32 v240, v240, s62, v95
	v_med3_f32 v241, v241, s62, v95
	v_mov_b32_e32 v242, 0
	v_mov_b32_e32 v243, 0
	v_mov_b32_e32 v244, 0
	v_mov_b32_e32 v245, 0
	v_cvt_pk_fp8_f32 v242, v226, v227
	v_cvt_pk_fp8_f32 v243, v230, v231
	v_cvt_pk_fp8_f32 v244, v234, v235
	v_cvt_pk_fp8_f32 v245, v238, v239
	v_cvt_pk_fp8_f32 v242, v228, v229 op_sel:[0,0,1]
	v_cvt_pk_fp8_f32 v243, v232, v233 op_sel:[0,0,1]
	v_cvt_pk_fp8_f32 v244, v236, v237 op_sel:[0,0,1]
	v_cvt_pk_fp8_f32 v245, v240, v241 op_sel:[0,0,1]
	s_nop 0
	global_store_dwordx4 v80, v[242:245], s[6:7]
	s_waitcnt vmcnt(12)
	v_mul_f32_e32 v144, v42, v144
	v_mul_f32_e32 v145, v42, v145
	v_mul_f32_e32 v146, v42, v146
	v_mul_f32_e32 v147, v42, v147
	ds_write_b128 v209, v[144:147]
	v_mul_f32_e32 v148, v43, v148
	v_mul_f32_e32 v149, v43, v149
	v_mul_f32_e32 v150, v43, v150
	v_mul_f32_e32 v151, v43, v151
	ds_write_b128 v209, v[148:151] offset:1024
	v_mul_f32_e32 v152, v44, v152
	v_mul_f32_e32 v153, v44, v153
	v_mul_f32_e32 v154, v44, v154
	v_mul_f32_e32 v155, v44, v155
	ds_write_b128 v209, v[152:155] offset:2048
	v_mul_f32_e32 v156, v45, v156
	v_mul_f32_e32 v157, v45, v157
	v_mul_f32_e32 v158, v45, v158
	v_mul_f32_e32 v159, v45, v159
	ds_write_b128 v209, v[156:159] offset:3072
	v_mul_f32_e32 v160, v46, v160
	v_mul_f32_e32 v161, v46, v161
	v_mul_f32_e32 v162, v46, v162
	v_mul_f32_e32 v163, v46, v163
	ds_write_b128 v209, v[160:163] offset:4096
	v_mul_f32_e32 v164, v47, v164
	v_mul_f32_e32 v165, v47, v165
	v_mul_f32_e32 v166, v47, v166
	v_mul_f32_e32 v167, v47, v167
	ds_write_b128 v209, v[164:167] offset:5120
	v_mul_f32_e32 v168, v48, v168
	v_mul_f32_e32 v169, v48, v169
	v_mul_f32_e32 v170, v48, v170
	v_mul_f32_e32 v171, v48, v171
	ds_write_b128 v209, v[168:171] offset:6144
	v_mul_f32_e32 v172, v49, v172
	v_mul_f32_e32 v173, v49, v173
	v_mul_f32_e32 v174, v49, v174
	v_mul_f32_e32 v175, v49, v175
	ds_write_b128 v209, v[172:175] offset:7168
	s_waitcnt lgkmcnt(0)
	s_barrier
; #define GAS __attribute__((address_space(1)))
; #define LAS __attribute__((address_space(3)))
; #define LDS_WAIT() asm volatile("s_waitcnt lgkmcnt(0)" ::: "memory")
; __device__ __forceinline__ unsigned pk2(float lo, float hi) { return f2bf(lo) | (f2bf(hi) << 16); }
; __device__ __forceinline__ int nat_dim(int p) { return (p >> 1) + 64 * (p & 1); }
; __device__ __forceinline__ int src_col_in(int c) {
;     if (c < 5120) { const int blk = c >> 7, p = c & 127; const bool rope = blk < 16 || ((((blk - 16) >> 2) & 1) == 0); const int d = rope ? (p >> 1) + 64 * (p & 1) : p; return blk * 128 + d; }
;     if (c < OFF_Z) return c + 2096;
;     if (c < OFF_G) return c - 4048;
;     if (c < OFF_DT) return 5120 + (c - OFF_G);
;     if (c < NSRC) return c;
;     return -1;
; }
; template <int MAP, bool KS, bool KPERM = false>
; __device__ __forceinline__ void p0_transpose_item(const float* W, int K, int Nsrc, int nblk, bf16* WT, const float* ksA, const float* ksB, int ksplit, LAS float* scr, int item, int lane) {
;     const int kb = item / nblk, nb = item % nblk, k0 = 64 * kb, n0 = 32 * nb;
;     const int nr = n0 + (lane & 31); const int sc = MAP == 1 ? src_col_in(nr) : (MAP == 2 ? nat_dim(nr) : nr);
;     float v[32];
; #pragma unroll
;     for (int i = 0; i < 32; ++i) { const int k = k0 + 2 * i + (lane >> 5); const int ksrc = KPERM ? ((k & ~127) + nat_dim(k & 127)) : k;
;         v[i] = sc >= 0 ? W[(size_t)ksrc * Nsrc + sc] : 0.f; }
; #pragma unroll
;     for (int i = 0; i < 32; ++i) { const int kk = 2 * i + (lane >> 5); const int k = k0 + kk;
;         if (KS) v[i] *= (k < ksplit ? ksA[k] : ksB[k - ksplit]);
;         scr[kk * 33 + (lane & 31)] = v[i]; }
;     LDS_WAIT(); asm volatile("" ::: "memory");
;     const int c = lane & 7;
; #pragma unroll
;     for (int j = 0; j < 4; ++j) { const int n = (lane >> 3) + 8 * j; const LAS float* s = scr + (8 * c) * 33 + n;
;         v4u o; o.x = pk2(s[0 * 33], s[1 * 33]); o.y = pk2(s[2 * 33], s[3 * 33]); o.z = pk2(s[4 * 33], s[5 * 33]); o.w = pk2(s[6 * 33], s[7 * 33]);
;         *(GAS v4u*)(WT + (size_t)(n0 + n) * K + k0 + 8 * c) = o; }
;     LDS_WAIT(); asm volatile("" ::: "memory");
; }
	s_add_i32 s24, s23, 16
	s_lshl_b32 s20, s24, 7
	s_cmp_lt_u32 s24, 40
	s_cselect_b32 s21, 0, 0x830
	s_cmp_lt_u32 s24, 72
	s_cselect_b32 s21, s21, 0xfffff030
	s_add_i32 s20, s20, s21
	s_lshl_b32 s20, s20, 2
	s_add_u32 s8, s46, s20
	s_addc_u32 s9, s47, 0
	global_load_dwordx4 v[144:147], v76, s[8:9]
	s_add_u32 s8, s8, 0x16280
	s_addc_u32 s9, s9, 0
	global_load_dwordx4 v[148:151], v76, s[8:9]
	s_add_u32 s8, s8, 0x16280
	s_addc_u32 s9, s9, 0
	global_load_dwordx4 v[152:155], v76, s[8:9]
	s_add_u32 s8, s8, 0x16280
	s_addc_u32 s9, s9, 0
	global_load_dwordx4 v[156:159], v76, s[8:9]
	s_add_u32 s8, s8, 0x16280
	s_addc_u32 s9, s9, 0
	global_load_dwordx4 v[160:163], v76, s[8:9]
	s_add_u32 s8, s8, 0x16280
	s_addc_u32 s9, s9, 0
	global_load_dwordx4 v[164:167], v76, s[8:9]
	s_add_u32 s8, s8, 0x16280
	s_addc_u32 s9, s9, 0
	global_load_dwordx4 v[168:171], v76, s[8:9]
	s_add_u32 s8, s8, 0x16280
	s_addc_u32 s9, s9, 0
	global_load_dwordx4 v[172:175], v76, s[8:9]
	s_add_i32 s24, s23, 0
	s_mul_i32 s20, s24, 0x100000
	s_add_u32 s6, s48, s20
	s_addc_u32 s7, s49, 0
	s_cmp_lt_u32 s24, 16
	s_cselect_b32 s20, 1, 0
	s_sub_i32 s21, s24, 16
	s_bitcmp0_b32 s21, 2
	s_cselect_b32 s21, 1, 0
	s_cmp_lt_u32 s24, 40
	s_cselect_b32 s21, s21, 0
	s_or_b32 s20, s20, s21
	s_cmp_lg_u32 s20, 0
	s_cselect_b64 s[20:21], -1, 0
	v_cndmask_b32_e64 v91, v83, v87, s[20:21]
	v_cndmask_b32_e64 v92, v84, v88, s[20:21]
	v_cndmask_b32_e64 v93, v85, v89, s[20:21]
	v_cndmask_b32_e64 v94, v86, v90, s[20:21]
	ds_read_b32 v226, v112
	ds_read_b32 v227, v112 offset:512
	ds_read_b32 v228, v112 offset:1024
	ds_read_b32 v229, v112 offset:1536
	ds_read_b32 v230, v112 offset:2048
	ds_read_b32 v231, v112 offset:2560
	ds_read_b32 v232, v112 offset:3072
	ds_read_b32 v233, v112 offset:3584
	s_waitcnt lgkmcnt(0)
	v_bfe_u32 v120, v226, 16, 1
	v_bfe_u32 v121, v227, 16, 1
	v_bfe_u32 v122, v228, 16, 1
	v_bfe_u32 v123, v229, 16, 1
	v_bfe_u32 v124, v230, 16, 1
	v_bfe_u32 v125, v231, 16, 1
	v_bfe_u32 v126, v232, 16, 1
	v_bfe_u32 v127, v233, 16, 1
	v_add3_u32 v226, v226, v120, s63
	v_add3_u32 v227, v227, v121, s63
	v_add3_u32 v228, v228, v122, s63
	v_add3_u32 v229, v229, v123, s63
	v_add3_u32 v230, v230, v124, s63
	v_add3_u32 v231, v231, v125, s63
	v_add3_u32 v232, v232, v126, s63
	v_add3_u32 v233, v233, v127, s63
	v_perm_b32 v242, v227, v226, s64
	v_perm_b32 v243, v229, v228, s64
	v_perm_b32 v244, v231, v230, s64
	v_perm_b32 v245, v233, v232, s64
	s_nop 0
	global_store_dwordx4 v91, v[242:245], s[6:7]
	ds_read_b32 v226, v114
	ds_read_b32 v227, v114 offset:512
	ds_read_b32 v228, v114 offset:1024
	ds_read_b32 v229, v114 offset:1536
	ds_read_b32 v230, v114 offset:2048
	ds_read_b32 v231, v114 offset:2560
	ds_read_b32 v232, v114 offset:3072
	ds_read_b32 v233, v114 offset:3584
	s_waitcnt lgkmcnt(0)
	v_bfe_u32 v120, v226, 16, 1
	v_bfe_u32 v121, v227, 16, 1
	v_bfe_u32 v122, v228, 16, 1
	v_bfe_u32 v123, v229, 16, 1
	v_bfe_u32 v124, v230, 16, 1
	v_bfe_u32 v125, v231, 16, 1
	v_bfe_u32 v126, v232, 16, 1
	v_bfe_u32 v127, v233, 16, 1
	v_add3_u32 v226, v226, v120, s63
	v_add3_u32 v227, v227, v121, s63
	v_add3_u32 v228, v228, v122, s63
	v_add3_u32 v229, v229, v123, s63
	v_add3_u32 v230, v230, v124, s63
	v_add3_u32 v231, v231, v125, s63
	v_add3_u32 v232, v232, v126, s63
	v_add3_u32 v233, v233, v127, s63
	v_perm_b32 v242, v227, v226, s64
	v_perm_b32 v243, v229, v228, s64
	v_perm_b32 v244, v231, v230, s64
	v_perm_b32 v245, v233, v232, s64
	s_nop 0
	global_store_dwordx4 v92, v[242:245], s[6:7]
	ds_read_b32 v226, v116
	ds_read_b32 v227, v116 offset:512
	ds_read_b32 v228, v116 offset:1024
	ds_read_b32 v229, v116 offset:1536
	ds_read_b32 v230, v116 offset:2048
	ds_read_b32 v231, v116 offset:2560
	ds_read_b32 v232, v116 offset:3072
	ds_read_b32 v233, v116 offset:3584
	s_waitcnt lgkmcnt(0)
	v_bfe_u32 v120, v226, 16, 1
	v_bfe_u32 v121, v227, 16, 1
	v_bfe_u32 v122, v228, 16, 1
	v_bfe_u32 v123, v229, 16, 1
	v_bfe_u32 v124, v230, 16, 1
	v_bfe_u32 v125, v231, 16, 1
	v_bfe_u32 v126, v232, 16, 1
	v_bfe_u32 v127, v233, 16, 1
	v_add3_u32 v226, v226, v120, s63
	v_add3_u32 v227, v227, v121, s63
	v_add3_u32 v228, v228, v122, s63
	v_add3_u32 v229, v229, v123, s63
	v_add3_u32 v230, v230, v124, s63
	v_add3_u32 v231, v231, v125, s63
	v_add3_u32 v232, v232, v126, s63
	v_add3_u32 v233, v233, v127, s63
	v_perm_b32 v242, v227, v226, s64
	v_perm_b32 v243, v229, v228, s64
	v_perm_b32 v244, v231, v230, s64
	v_perm_b32 v245, v233, v232, s64
	s_nop 0
	global_store_dwordx4 v93, v[242:245], s[6:7]
	ds_read_b32 v226, v118
	ds_read_b32 v227, v118 offset:512
	ds_read_b32 v228, v118 offset:1024
	ds_read_b32 v229, v118 offset:1536
	ds_read_b32 v230, v118 offset:2048
	ds_read_b32 v231, v118 offset:2560
	ds_read_b32 v232, v118 offset:3072
	ds_read_b32 v233, v118 offset:3584
	s_waitcnt lgkmcnt(0)
	v_bfe_u32 v120, v226, 16, 1
	v_bfe_u32 v121, v227, 16, 1
	v_bfe_u32 v122, v228, 16, 1
	v_bfe_u32 v123, v229, 16, 1
	v_bfe_u32 v124, v230, 16, 1
	v_bfe_u32 v125, v231, 16, 1
	v_bfe_u32 v126, v232, 16, 1
	v_bfe_u32 v127, v233, 16, 1
	v_add3_u32 v226, v226, v120, s63
	v_add3_u32 v227, v227, v121, s63
	v_add3_u32 v228, v228, v122, s63
	v_add3_u32 v229, v229, v123, s63
	v_add3_u32 v230, v230, v124, s63
	v_add3_u32 v231, v231, v125, s63
	v_add3_u32 v232, v232, v126, s63
	v_add3_u32 v233, v233, v127, s63
	v_perm_b32 v242, v227, v226, s64
	v_perm_b32 v243, v229, v228, s64
	v_perm_b32 v244, v231, v230, s64
	v_perm_b32 v245, v233, v232, s64
	s_nop 0
	global_store_dwordx4 v94, v[242:245], s[6:7]
	s_waitcnt vmcnt(14)
	v_mul_f32_e32 v176, v42, v176
	v_mul_f32_e32 v177, v42, v177
	v_mul_f32_e32 v178, v42, v178
	v_mul_f32_e32 v179, v42, v179
	ds_write_b128 v210, v[176:179]
	v_mul_f32_e32 v180, v43, v180
	v_mul_f32_e32 v181, v43, v181
	v_mul_f32_e32 v182, v43, v182
	v_mul_f32_e32 v183, v43, v183
	ds_write_b128 v210, v[180:183] offset:1024
	v_mul_f32_e32 v184, v44, v184
	v_mul_f32_e32 v185, v44, v185
	v_mul_f32_e32 v186, v44, v186
	v_mul_f32_e32 v187, v44, v187
	ds_write_b128 v210, v[184:187] offset:2048
	v_mul_f32_e32 v188, v45, v188
	v_mul_f32_e32 v189, v45, v189
	v_mul_f32_e32 v190, v45, v190
	v_mul_f32_e32 v191, v45, v191
	ds_write_b128 v210, v[188:191] offset:3072
	v_mul_f32_e32 v192, v46, v192
	v_mul_f32_e32 v193, v46, v193
	v_mul_f32_e32 v194, v46, v194
	v_mul_f32_e32 v195, v46, v195
	ds_write_b128 v210, v[192:195] offset:4096
	v_mul_f32_e32 v196, v47, v196
	v_mul_f32_e32 v197, v47, v197
	v_mul_f32_e32 v198, v47, v198
	v_mul_f32_e32 v199, v47, v199
	ds_write_b128 v210, v[196:199] offset:5120
	v_mul_f32_e32 v200, v48, v200
	v_mul_f32_e32 v201, v48, v201
	v_mul_f32_e32 v202, v48, v202
	v_mul_f32_e32 v203, v48, v203
	ds_write_b128 v210, v[200:203] offset:6144
	v_mul_f32_e32 v204, v49, v204
	v_mul_f32_e32 v205, v49, v205
	v_mul_f32_e32 v206, v49, v206
	v_mul_f32_e32 v207, v49, v207
	ds_write_b128 v210, v[204:207] offset:7168
	s_waitcnt lgkmcnt(0)
	s_barrier
; #define GAS __attribute__((address_space(1)))
; #define LAS __attribute__((address_space(3)))
; #define LDS_WAIT() asm volatile("s_waitcnt lgkmcnt(0)" ::: "memory")
; __device__ __forceinline__ unsigned pk2(float lo, float hi) { return f2bf(lo) | (f2bf(hi) << 16); }
; __device__ __forceinline__ int nat_dim(int p) { return (p >> 1) + 64 * (p & 1); }
; __device__ __forceinline__ int src_col_in(int c) {
;     if (c < 5120) { const int blk = c >> 7, p = c & 127; const bool rope = blk < 16 || ((((blk - 16) >> 2) & 1) == 0); const int d = rope ? (p >> 1) + 64 * (p & 1) : p; return blk * 128 + d; }
;     if (c < OFF_Z) return c + 2096;
;     if (c < OFF_G) return c - 4048;
;     if (c < OFF_DT) return 5120 + (c - OFF_G);
;     if (c < NSRC) return c;
;     return -1;
; }
; template <int MAP, bool KS, bool KPERM = false>
; __device__ __forceinline__ void p0_transpose_item(const float* W, int K, int Nsrc, int nblk, bf16* WT, const float* ksA, const float* ksB, int ksplit, LAS float* scr, int item, int lane) {
;     const int kb = item / nblk, nb = item % nblk, k0 = 64 * kb, n0 = 32 * nb;
;     const int nr = n0 + (lane & 31); const int sc = MAP == 1 ? src_col_in(nr) : (MAP == 2 ? nat_dim(nr) : nr);
;     float v[32];
; #pragma unroll
;     for (int i = 0; i < 32; ++i) { const int k = k0 + 2 * i + (lane >> 5); const int ksrc = KPERM ? ((k & ~127) + nat_dim(k & 127)) : k;
;         v[i] = sc >= 0 ? W[(size_t)ksrc * Nsrc + sc] : 0.f; }
; #pragma unroll
;     for (int i = 0; i < 32; ++i) { const int kk = 2 * i + (lane >> 5); const int k = k0 + kk;
;         if (KS) v[i] *= (k < ksplit ? ksA[k] : ksB[k - ksplit]);
;         scr[kk * 33 + (lane & 31)] = v[i]; }
;     LDS_WAIT(); asm volatile("" ::: "memory");
;     const int c = lane & 7;
; #pragma unroll
;     for (int j = 0; j < 4; ++j) { const int n = (lane >> 3) + 8 * j; const LAS float* s = scr + (8 * c) * 33 + n;
;         v4u o; o.x = pk2(s[0 * 33], s[1 * 33]); o.y = pk2(s[2 * 33], s[3 * 33]); o.z = pk2(s[4 * 33], s[5 * 33]); o.w = pk2(s[6 * 33], s[7 * 33]);
;         *(GAS v4u*)(WT + (size_t)(n0 + n) * K + k0 + 8 * c) = o; }
;     LDS_WAIT(); asm volatile("" ::: "memory");
; }
	s_add_i32 s24, s23, 24
	s_lshl_b32 s20, s24, 7
	s_cmp_lt_u32 s24, 40
	s_cselect_b32 s21, 0, 0x830
	s_cmp_lt_u32 s24, 72
	s_cselect_b32 s21, s21, 0xfffff030
	s_add_i32 s20, s20, s21
	s_lshl_b32 s20, s20, 2
	s_add_u32 s8, s46, s20
	s_addc_u32 s9, s47, 0
	global_load_dwordx4 v[176:179], v76, s[8:9]
	s_add_u32 s8, s8, 0x16280
	s_addc_u32 s9, s9, 0
	global_load_dwordx4 v[180:183], v76, s[8:9]
	s_add_u32 s8, s8, 0x16280
	s_addc_u32 s9, s9, 0
	global_load_dwordx4 v[184:187], v76, s[8:9]
	s_add_u32 s8, s8, 0x16280
	s_addc_u32 s9, s9, 0
	global_load_dwordx4 v[188:191], v76, s[8:9]
	s_add_u32 s8, s8, 0x16280
	s_addc_u32 s9, s9, 0
	global_load_dwordx4 v[192:195], v76, s[8:9]
	s_add_u32 s8, s8, 0x16280
	s_addc_u32 s9, s9, 0
	global_load_dwordx4 v[196:199], v76, s[8:9]
	s_add_u32 s8, s8, 0x16280
	s_addc_u32 s9, s9, 0
	global_load_dwordx4 v[200:203], v76, s[8:9]
	s_add_u32 s8, s8, 0x16280
	s_addc_u32 s9, s9, 0
	global_load_dwordx4 v[204:207], v76, s[8:9]
	s_add_i32 s24, s23, 8
	s_mul_i32 s20, s24, 0x100000
	s_add_u32 s6, s48, s20
	s_addc_u32 s7, s49, 0
	s_cmp_lt_u32 s24, 16
	s_cselect_b32 s20, 1, 0
	s_sub_i32 s21, s24, 16
	s_bitcmp0_b32 s21, 2
	s_cselect_b32 s21, 1, 0
	s_cmp_lt_u32 s24, 40
	s_cselect_b32 s21, s21, 0
	s_or_b32 s20, s20, s21
	s_cmp_lg_u32 s20, 0
	s_cselect_b64 s[20:21], -1, 0
	v_cndmask_b32_e64 v91, v83, v87, s[20:21]
	v_cndmask_b32_e64 v92, v84, v88, s[20:21]
	v_cndmask_b32_e64 v93, v85, v89, s[20:21]
	v_cndmask_b32_e64 v94, v86, v90, s[20:21]
	ds_read_b32 v226, v113
	ds_read_b32 v227, v113 offset:512
	ds_read_b32 v228, v113 offset:1024
	ds_read_b32 v229, v113 offset:1536
	ds_read_b32 v230, v113 offset:2048
	ds_read_b32 v231, v113 offset:2560
	ds_read_b32 v232, v113 offset:3072
	ds_read_b32 v233, v113 offset:3584
	s_waitcnt lgkmcnt(0)
	v_bfe_u32 v120, v226, 16, 1
	v_bfe_u32 v121, v227, 16, 1
	v_bfe_u32 v122, v228, 16, 1
	v_bfe_u32 v123, v229, 16, 1
	v_bfe_u32 v124, v230, 16, 1
	v_bfe_u32 v125, v231, 16, 1
	v_bfe_u32 v126, v232, 16, 1
	v_bfe_u32 v127, v233, 16, 1
	v_add3_u32 v226, v226, v120, s63
	v_add3_u32 v227, v227, v121, s63
	v_add3_u32 v228, v228, v122, s63
	v_add3_u32 v229, v229, v123, s63
	v_add3_u32 v230, v230, v124, s63
	v_add3_u32 v231, v231, v125, s63
	v_add3_u32 v232, v232, v126, s63
	v_add3_u32 v233, v233, v127, s63
	v_perm_b32 v242, v227, v226, s64
	v_perm_b32 v243, v229, v228, s64
	v_perm_b32 v244, v231, v230, s64
	v_perm_b32 v245, v233, v232, s64
	s_nop 0
	global_store_dwordx4 v91, v[242:245], s[6:7]
	ds_read_b32 v226, v115
	ds_read_b32 v227, v115 offset:512
	ds_read_b32 v228, v115 offset:1024
	ds_read_b32 v229, v115 offset:1536
	ds_read_b32 v230, v115 offset:2048
	ds_read_b32 v231, v115 offset:2560
	ds_read_b32 v232, v115 offset:3072
	ds_read_b32 v233, v115 offset:3584
	s_waitcnt lgkmcnt(0)
	v_bfe_u32 v120, v226, 16, 1
	v_bfe_u32 v121, v227, 16, 1
	v_bfe_u32 v122, v228, 16, 1
	v_bfe_u32 v123, v229, 16, 1
	v_bfe_u32 v124, v230, 16, 1
	v_bfe_u32 v125, v231, 16, 1
	v_bfe_u32 v126, v232, 16, 1
	v_bfe_u32 v127, v233, 16, 1
	v_add3_u32 v226, v226, v120, s63
	v_add3_u32 v227, v227, v121, s63
	v_add3_u32 v228, v228, v122, s63
	v_add3_u32 v229, v229, v123, s63
	v_add3_u32 v230, v230, v124, s63
	v_add3_u32 v231, v231, v125, s63
	v_add3_u32 v232, v232, v126, s63
	v_add3_u32 v233, v233, v127, s63
	v_perm_b32 v242, v227, v226, s64
	v_perm_b32 v243, v229, v228, s64
	v_perm_b32 v244, v231, v230, s64
	v_perm_b32 v245, v233, v232, s64
	s_nop 0
	global_store_dwordx4 v92, v[242:245], s[6:7]
	ds_read_b32 v226, v117
	ds_read_b32 v227, v117 offset:512
	ds_read_b32 v228, v117 offset:1024
	ds_read_b32 v229, v117 offset:1536
	ds_read_b32 v230, v117 offset:2048
	ds_read_b32 v231, v117 offset:2560
	ds_read_b32 v232, v117 offset:3072
	ds_read_b32 v233, v117 offset:3584
	s_waitcnt lgkmcnt(0)
	v_bfe_u32 v120, v226, 16, 1
	v_bfe_u32 v121, v227, 16, 1
	v_bfe_u32 v122, v228, 16, 1
	v_bfe_u32 v123, v229, 16, 1
	v_bfe_u32 v124, v230, 16, 1
	v_bfe_u32 v125, v231, 16, 1
	v_bfe_u32 v126, v232, 16, 1
	v_bfe_u32 v127, v233, 16, 1
	v_add3_u32 v226, v226, v120, s63
	v_add3_u32 v227, v227, v121, s63
	v_add3_u32 v228, v228, v122, s63
	v_add3_u32 v229, v229, v123, s63
	v_add3_u32 v230, v230, v124, s63
	v_add3_u32 v231, v231, v125, s63
	v_add3_u32 v232, v232, v126, s63
	v_add3_u32 v233, v233, v127, s63
	v_perm_b32 v242, v227, v226, s64
	v_perm_b32 v243, v229, v228, s64
	v_perm_b32 v244, v231, v230, s64
	v_perm_b32 v245, v233, v232, s64
	s_nop 0
	global_store_dwordx4 v93, v[242:245], s[6:7]
	ds_read_b32 v226, v119
	ds_read_b32 v227, v119 offset:512
	ds_read_b32 v228, v119 offset:1024
	ds_read_b32 v229, v119 offset:1536
	ds_read_b32 v230, v119 offset:2048
	ds_read_b32 v231, v119 offset:2560
	ds_read_b32 v232, v119 offset:3072
	ds_read_b32 v233, v119 offset:3584
	s_waitcnt lgkmcnt(0)
	v_bfe_u32 v120, v226, 16, 1
	v_bfe_u32 v121, v227, 16, 1
	v_bfe_u32 v122, v228, 16, 1
	v_bfe_u32 v123, v229, 16, 1
	v_bfe_u32 v124, v230, 16, 1
	v_bfe_u32 v125, v231, 16, 1
	v_bfe_u32 v126, v232, 16, 1
	v_bfe_u32 v127, v233, 16, 1
	v_add3_u32 v226, v226, v120, s63
	v_add3_u32 v227, v227, v121, s63
	v_add3_u32 v228, v228, v122, s63
	v_add3_u32 v229, v229, v123, s63
	v_add3_u32 v230, v230, v124, s63
	v_add3_u32 v231, v231, v125, s63
	v_add3_u32 v232, v232, v126, s63
	v_add3_u32 v233, v233, v127, s63
	v_perm_b32 v242, v227, v226, s64
	v_perm_b32 v243, v229, v228, s64
	v_perm_b32 v244, v231, v230, s64
	v_perm_b32 v245, v233, v232, s64
	s_nop 0
	global_store_dwordx4 v94, v[242:245], s[6:7]
	s_waitcnt vmcnt(16)
	v_mul_f32_e32 v144, v42, v144
	v_mul_f32_e32 v145, v42, v145
	v_mul_f32_e32 v146, v42, v146
	v_mul_f32_e32 v147, v42, v147
	ds_write_b128 v209, v[144:147]
	v_mul_f32_e32 v148, v43, v148
	v_mul_f32_e32 v149, v43, v149
	v_mul_f32_e32 v150, v43, v150
	v_mul_f32_e32 v151, v43, v151
	ds_write_b128 v209, v[148:151] offset:1024
	v_mul_f32_e32 v152, v44, v152
	v_mul_f32_e32 v153, v44, v153
	v_mul_f32_e32 v154, v44, v154
	v_mul_f32_e32 v155, v44, v155
	ds_write_b128 v209, v[152:155] offset:2048
	v_mul_f32_e32 v156, v45, v156
	v_mul_f32_e32 v157, v45, v157
	v_mul_f32_e32 v158, v45, v158
	v_mul_f32_e32 v159, v45, v159
	ds_write_b128 v209, v[156:159] offset:3072
	v_mul_f32_e32 v160, v46, v160
	v_mul_f32_e32 v161, v46, v161
	v_mul_f32_e32 v162, v46, v162
	v_mul_f32_e32 v163, v46, v163
	ds_write_b128 v209, v[160:163] offset:4096
	v_mul_f32_e32 v164, v47, v164
	v_mul_f32_e32 v165, v47, v165
	v_mul_f32_e32 v166, v47, v166
	v_mul_f32_e32 v167, v47, v167
	ds_write_b128 v209, v[164:167] offset:5120
	v_mul_f32_e32 v168, v48, v168
	v_mul_f32_e32 v169, v48, v169
	v_mul_f32_e32 v170, v48, v170
	v_mul_f32_e32 v171, v48, v171
	ds_write_b128 v209, v[168:171] offset:6144
	v_mul_f32_e32 v172, v49, v172
	v_mul_f32_e32 v173, v49, v173
	v_mul_f32_e32 v174, v49, v174
	v_mul_f32_e32 v175, v49, v175
	ds_write_b128 v209, v[172:175] offset:7168
	s_waitcnt lgkmcnt(0)
	s_barrier
; #define GAS __attribute__((address_space(1)))
; #define LAS __attribute__((address_space(3)))
; #define LDS_WAIT() asm volatile("s_waitcnt lgkmcnt(0)" ::: "memory")
; __device__ __forceinline__ unsigned pk2(float lo, float hi) { return f2bf(lo) | (f2bf(hi) << 16); }
; __device__ __forceinline__ int nat_dim(int p) { return (p >> 1) + 64 * (p & 1); }
; __device__ __forceinline__ int src_col_in(int c) {
;     if (c < 5120) { const int blk = c >> 7, p = c & 127; const bool rope = blk < 16 || ((((blk - 16) >> 2) & 1) == 0); const int d = rope ? (p >> 1) + 64 * (p & 1) : p; return blk * 128 + d; }
;     if (c < OFF_Z) return c + 2096;
;     if (c < OFF_G) return c - 4048;
;     if (c < OFF_DT) return 5120 + (c - OFF_G);
;     if (c < NSRC) return c;
;     return -1;
; }
; template <int MAP, bool KS, bool KPERM = false>
; __device__ __forceinline__ void p0_transpose_item(const float* W, int K, int Nsrc, int nblk, bf16* WT, const float* ksA, const float* ksB, int ksplit, LAS float* scr, int item, int lane) {
;     const int kb = item / nblk, nb = item % nblk, k0 = 64 * kb, n0 = 32 * nb;
;     const int nr = n0 + (lane & 31); const int sc = MAP == 1 ? src_col_in(nr) : (MAP == 2 ? nat_dim(nr) : nr);
;     float v[32];
; #pragma unroll
;     for (int i = 0; i < 32; ++i) { const int k = k0 + 2 * i + (lane >> 5); const int ksrc = KPERM ? ((k & ~127) + nat_dim(k & 127)) : k;
;         v[i] = sc >= 0 ? W[(size_t)ksrc * Nsrc + sc] : 0.f; }
; #pragma unroll
;     for (int i = 0; i < 32; ++i) { const int kk = 2 * i + (lane >> 5); const int k = k0 + kk;
;         if (KS) v[i] *= (k < ksplit ? ksA[k] : ksB[k - ksplit]);
;         scr[kk * 33 + (lane & 31)] = v[i]; }
;     LDS_WAIT(); asm volatile("" ::: "memory");
;     const int c = lane & 7;
; #pragma unroll
;     for (int j = 0; j < 4; ++j) { const int n = (lane >> 3) + 8 * j; const LAS float* s = scr + (8 * c) * 33 + n;
;         v4u o; o.x = pk2(s[0 * 33], s[1 * 33]); o.y = pk2(s[2 * 33], s[3 * 33]); o.z = pk2(s[4 * 33], s[5 * 33]); o.w = pk2(s[6 * 33], s[7 * 33]);
;         *(GAS v4u*)(WT + (size_t)(n0 + n) * K + k0 + 8 * c) = o; }
;     LDS_WAIT(); asm volatile("" ::: "memory");
; }
	s_add_i32 s24, s23, 32
	s_lshl_b32 s20, s24, 7
	s_cmp_lt_u32 s24, 40
	s_cselect_b32 s21, 0, 0x830
	s_cmp_lt_u32 s24, 72
	s_cselect_b32 s21, s21, 0xfffff030
	s_add_i32 s20, s20, s21
	s_lshl_b32 s20, s20, 2
	s_add_u32 s8, s46, s20
	s_addc_u32 s9, s47, 0
	global_load_dwordx4 v[144:147], v76, s[8:9]
	s_add_u32 s8, s8, 0x16280
	s_addc_u32 s9, s9, 0
	global_load_dwordx4 v[148:151], v76, s[8:9]
	s_add_u32 s8, s8, 0x16280
	s_addc_u32 s9, s9, 0
	global_load_dwordx4 v[152:155], v76, s[8:9]
	s_add_u32 s8, s8, 0x16280
	s_addc_u32 s9, s9, 0
	global_load_dwordx4 v[156:159], v76, s[8:9]
	s_add_u32 s8, s8, 0x16280
	s_addc_u32 s9, s9, 0
	global_load_dwordx4 v[160:163], v76, s[8:9]
	s_add_u32 s8, s8, 0x16280
	s_addc_u32 s9, s9, 0
	global_load_dwordx4 v[164:167], v76, s[8:9]
	s_add_u32 s8, s8, 0x16280
	s_addc_u32 s9, s9, 0
	global_load_dwordx4 v[168:171], v76, s[8:9]
	s_add_u32 s8, s8, 0x16280
	s_addc_u32 s9, s9, 0
	global_load_dwordx4 v[172:175], v76, s[8:9]
	s_add_i32 s24, s23, 16
	s_mul_i32 s20, s24, 0x100000
	s_add_u32 s6, s48, s20
	s_addc_u32 s7, s49, 0
	s_cmp_lt_u32 s24, 16
	s_cselect_b32 s20, 1, 0
	s_sub_i32 s21, s24, 16
	s_bitcmp0_b32 s21, 2
	s_cselect_b32 s21, 1, 0
	s_cmp_lt_u32 s24, 40
	s_cselect_b32 s21, s21, 0
	s_or_b32 s20, s20, s21
	s_cmp_lg_u32 s20, 0
	s_cselect_b64 s[20:21], -1, 0
	v_cndmask_b32_e64 v91, v83, v87, s[20:21]
	v_cndmask_b32_e64 v92, v84, v88, s[20:21]
	v_cndmask_b32_e64 v93, v85, v89, s[20:21]
	v_cndmask_b32_e64 v94, v86, v90, s[20:21]
	ds_read_b32 v226, v112
	ds_read_b32 v227, v112 offset:512
	ds_read_b32 v228, v112 offset:1024
	ds_read_b32 v229, v112 offset:1536
	ds_read_b32 v230, v112 offset:2048
	ds_read_b32 v231, v112 offset:2560
	ds_read_b32 v232, v112 offset:3072
	ds_read_b32 v233, v112 offset:3584
	s_waitcnt lgkmcnt(0)
	v_bfe_u32 v120, v226, 16, 1
	v_bfe_u32 v121, v227, 16, 1
	v_bfe_u32 v122, v228, 16, 1
	v_bfe_u32 v123, v229, 16, 1
	v_bfe_u32 v124, v230, 16, 1
	v_bfe_u32 v125, v231, 16, 1
	v_bfe_u32 v126, v232, 16, 1
	v_bfe_u32 v127, v233, 16, 1
	v_add3_u32 v226, v226, v120, s63
	v_add3_u32 v227, v227, v121, s63
	v_add3_u32 v228, v228, v122, s63
	v_add3_u32 v229, v229, v123, s63
	v_add3_u32 v230, v230, v124, s63
	v_add3_u32 v231, v231, v125, s63
	v_add3_u32 v232, v232, v126, s63
	v_add3_u32 v233, v233, v127, s63
	v_perm_b32 v242, v227, v226, s64
	v_perm_b32 v243, v229, v228, s64
	v_perm_b32 v244, v231, v230, s64
	v_perm_b32 v245, v233, v232, s64
	s_nop 0
	global_store_dwordx4 v91, v[242:245], s[6:7]
	ds_read_b32 v226, v114
	ds_read_b32 v227, v114 offset:512
	ds_read_b32 v228, v114 offset:1024
	ds_read_b32 v229, v114 offset:1536
	ds_read_b32 v230, v114 offset:2048
	ds_read_b32 v231, v114 offset:2560
	ds_read_b32 v232, v114 offset:3072
	ds_read_b32 v233, v114 offset:3584
	s_waitcnt lgkmcnt(0)
	v_bfe_u32 v120, v226, 16, 1
	v_bfe_u32 v121, v227, 16, 1
	v_bfe_u32 v122, v228, 16, 1
	v_bfe_u32 v123, v229, 16, 1
	v_bfe_u32 v124, v230, 16, 1
	v_bfe_u32 v125, v231, 16, 1
	v_bfe_u32 v126, v232, 16, 1
	v_bfe_u32 v127, v233, 16, 1
	v_add3_u32 v226, v226, v120, s63
	v_add3_u32 v227, v227, v121, s63
	v_add3_u32 v228, v228, v122, s63
	v_add3_u32 v229, v229, v123, s63
	v_add3_u32 v230, v230, v124, s63
	v_add3_u32 v231, v231, v125, s63
	v_add3_u32 v232, v232, v126, s63
	v_add3_u32 v233, v233, v127, s63
	v_perm_b32 v242, v227, v226, s64
	v_perm_b32 v243, v229, v228, s64
	v_perm_b32 v244, v231, v230, s64
	v_perm_b32 v245, v233, v232, s64
	s_nop 0
	global_store_dwordx4 v92, v[242:245], s[6:7]
	ds_read_b32 v226, v116
	ds_read_b32 v227, v116 offset:512
	ds_read_b32 v228, v116 offset:1024
	ds_read_b32 v229, v116 offset:1536
	ds_read_b32 v230, v116 offset:2048
	ds_read_b32 v231, v116 offset:2560
	ds_read_b32 v232, v116 offset:3072
	ds_read_b32 v233, v116 offset:3584
	s_waitcnt lgkmcnt(0)
	v_bfe_u32 v120, v226, 16, 1
	v_bfe_u32 v121, v227, 16, 1
	v_bfe_u32 v122, v228, 16, 1
	v_bfe_u32 v123, v229, 16, 1
	v_bfe_u32 v124, v230, 16, 1
	v_bfe_u32 v125, v231, 16, 1
	v_bfe_u32 v126, v232, 16, 1
	v_bfe_u32 v127, v233, 16, 1
	v_add3_u32 v226, v226, v120, s63
	v_add3_u32 v227, v227, v121, s63
	v_add3_u32 v228, v228, v122, s63
	v_add3_u32 v229, v229, v123, s63
	v_add3_u32 v230, v230, v124, s63
	v_add3_u32 v231, v231, v125, s63
	v_add3_u32 v232, v232, v126, s63
	v_add3_u32 v233, v233, v127, s63
	v_perm_b32 v242, v227, v226, s64
	v_perm_b32 v243, v229, v228, s64
	v_perm_b32 v244, v231, v230, s64
	v_perm_b32 v245, v233, v232, s64
	s_nop 0
	global_store_dwordx4 v93, v[242:245], s[6:7]
	ds_read_b32 v226, v118
	ds_read_b32 v227, v118 offset:512
	ds_read_b32 v228, v118 offset:1024
	ds_read_b32 v229, v118 offset:1536
	ds_read_b32 v230, v118 offset:2048
	ds_read_b32 v231, v118 offset:2560
	ds_read_b32 v232, v118 offset:3072
	ds_read_b32 v233, v118 offset:3584
	s_waitcnt lgkmcnt(0)
	v_bfe_u32 v120, v226, 16, 1
	v_bfe_u32 v121, v227, 16, 1
	v_bfe_u32 v122, v228, 16, 1
	v_bfe_u32 v123, v229, 16, 1
	v_bfe_u32 v124, v230, 16, 1
	v_bfe_u32 v125, v231, 16, 1
	v_bfe_u32 v126, v232, 16, 1
	v_bfe_u32 v127, v233, 16, 1
	v_add3_u32 v226, v226, v120, s63
	v_add3_u32 v227, v227, v121, s63
	v_add3_u32 v228, v228, v122, s63
	v_add3_u32 v229, v229, v123, s63
	v_add3_u32 v230, v230, v124, s63
	v_add3_u32 v231, v231, v125, s63
	v_add3_u32 v232, v232, v126, s63
	v_add3_u32 v233, v233, v127, s63
	v_perm_b32 v242, v227, v226, s64
	v_perm_b32 v243, v229, v228, s64
	v_perm_b32 v244, v231, v230, s64
	v_perm_b32 v245, v233, v232, s64
	s_nop 0
	global_store_dwordx4 v94, v[242:245], s[6:7]
	s_waitcnt vmcnt(16)
	v_mul_f32_e32 v176, v42, v176
	v_mul_f32_e32 v177, v42, v177
	v_mul_f32_e32 v178, v42, v178
	v_mul_f32_e32 v179, v42, v179
	ds_write_b128 v210, v[176:179]
	v_mul_f32_e32 v180, v43, v180
	v_mul_f32_e32 v181, v43, v181
	v_mul_f32_e32 v182, v43, v182
	v_mul_f32_e32 v183, v43, v183
	ds_write_b128 v210, v[180:183] offset:1024
	v_mul_f32_e32 v184, v44, v184
	v_mul_f32_e32 v185, v44, v185
	v_mul_f32_e32 v186, v44, v186
	v_mul_f32_e32 v187, v44, v187
	ds_write_b128 v210, v[184:187] offset:2048
	v_mul_f32_e32 v188, v45, v188
	v_mul_f32_e32 v189, v45, v189
	v_mul_f32_e32 v190, v45, v190
	v_mul_f32_e32 v191, v45, v191
	ds_write_b128 v210, v[188:191] offset:3072
	v_mul_f32_e32 v192, v46, v192
	v_mul_f32_e32 v193, v46, v193
	v_mul_f32_e32 v194, v46, v194
	v_mul_f32_e32 v195, v46, v195
	ds_write_b128 v210, v[192:195] offset:4096
	v_mul_f32_e32 v196, v47, v196
	v_mul_f32_e32 v197, v47, v197
	v_mul_f32_e32 v198, v47, v198
	v_mul_f32_e32 v199, v47, v199
	ds_write_b128 v210, v[196:199] offset:5120
	v_mul_f32_e32 v200, v48, v200
	v_mul_f32_e32 v201, v48, v201
	v_mul_f32_e32 v202, v48, v202
	v_mul_f32_e32 v203, v48, v203
	ds_write_b128 v210, v[200:203] offset:6144
	v_mul_f32_e32 v204, v49, v204
	v_mul_f32_e32 v205, v49, v205
	v_mul_f32_e32 v206, v49, v206
	v_mul_f32_e32 v207, v49, v207
	ds_write_b128 v210, v[204:207] offset:7168
	s_waitcnt lgkmcnt(0)
	s_barrier
; #define GAS __attribute__((address_space(1)))
; #define LAS __attribute__((address_space(3)))
; #define LDS_WAIT() asm volatile("s_waitcnt lgkmcnt(0)" ::: "memory")
; __device__ __forceinline__ unsigned pk2(float lo, float hi) { return f2bf(lo) | (f2bf(hi) << 16); }
; __device__ __forceinline__ int nat_dim(int p) { return (p >> 1) + 64 * (p & 1); }
; __device__ __forceinline__ int src_col_in(int c) {
;     if (c < 5120) { const int blk = c >> 7, p = c & 127; const bool rope = blk < 16 || ((((blk - 16) >> 2) & 1) == 0); const int d = rope ? (p >> 1) + 64 * (p & 1) : p; return blk * 128 + d; }
;     if (c < OFF_Z) return c + 2096;
;     if (c < OFF_G) return c - 4048;
;     if (c < OFF_DT) return 5120 + (c - OFF_G);
;     if (c < NSRC) return c;
;     return -1;
; }
; template <int MAP, bool KS, bool KPERM = false>
; __device__ __forceinline__ void p0_transpose_item(const float* W, int K, int Nsrc, int nblk, bf16* WT, const float* ksA, const float* ksB, int ksplit, LAS float* scr, int item, int lane) {
;     const int kb = item / nblk, nb = item % nblk, k0 = 64 * kb, n0 = 32 * nb;
;     const int nr = n0 + (lane & 31); const int sc = MAP == 1 ? src_col_in(nr) : (MAP == 2 ? nat_dim(nr) : nr);
;     float v[32];
; #pragma unroll
;     for (int i = 0; i < 32; ++i) { const int k = k0 + 2 * i + (lane >> 5); const int ksrc = KPERM ? ((k & ~127) + nat_dim(k & 127)) : k;
;         v[i] = sc >= 0 ? W[(size_t)ksrc * Nsrc + sc] : 0.f; }
; #pragma unroll
;     for (int i = 0; i < 32; ++i) { const int kk = 2 * i + (lane >> 5); const int k = k0 + kk;
;         if (KS) v[i] *= (k < ksplit ? ksA[k] : ksB[k - ksplit]);
;         scr[kk * 33 + (lane & 31)] = v[i]; }
;     LDS_WAIT(); asm volatile("" ::: "memory");
;     const int c = lane & 7;
; #pragma unroll
;     for (int j = 0; j < 4; ++j) { const int n = (lane >> 3) + 8 * j; const LAS float* s = scr + (8 * c) * 33 + n;
;         v4u o; o.x = pk2(s[0 * 33], s[1 * 33]); o.y = pk2(s[2 * 33], s[3 * 33]); o.z = pk2(s[4 * 33], s[5 * 33]); o.w = pk2(s[6 * 33], s[7 * 33]);
;         *(GAS v4u*)(WT + (size_t)(n0 + n) * K + k0 + 8 * c) = o; }
;     LDS_WAIT(); asm volatile("" ::: "memory");
; }
	s_add_i32 s24, s23, 40
	s_lshl_b32 s20, s24, 7
	s_cmp_lt_u32 s24, 40
	s_cselect_b32 s21, 0, 0x830
	s_cmp_lt_u32 s24, 72
	s_cselect_b32 s21, s21, 0xfffff030
	s_add_i32 s20, s20, s21
	s_lshl_b32 s20, s20, 2
	s_add_u32 s8, s46, s20
	s_addc_u32 s9, s47, 0
	global_load_dwordx4 v[176:179], v76, s[8:9]
	s_add_u32 s8, s8, 0x16280
	s_addc_u32 s9, s9, 0
	global_load_dwordx4 v[180:183], v76, s[8:9]
	s_add_u32 s8, s8, 0x16280
	s_addc_u32 s9, s9, 0
	global_load_dwordx4 v[184:187], v76, s[8:9]
	s_add_u32 s8, s8, 0x16280
	s_addc_u32 s9, s9, 0
	global_load_dwordx4 v[188:191], v76, s[8:9]
	s_add_u32 s8, s8, 0x16280
	s_addc_u32 s9, s9, 0
	global_load_dwordx4 v[192:195], v76, s[8:9]
	s_add_u32 s8, s8, 0x16280
	s_addc_u32 s9, s9, 0
	global_load_dwordx4 v[196:199], v76, s[8:9]
	s_add_u32 s8, s8, 0x16280
	s_addc_u32 s9, s9, 0
	global_load_dwordx4 v[200:203], v76, s[8:9]
	s_add_u32 s8, s8, 0x16280
	s_addc_u32 s9, s9, 0
	global_load_dwordx4 v[204:207], v76, s[8:9]
	s_add_i32 s24, s23, 24
	s_mul_i32 s20, s24, 0x100000
	s_add_u32 s6, s48, s20
	s_addc_u32 s7, s49, 0
	s_cmp_lt_u32 s24, 16
	s_cselect_b32 s20, 1, 0
	s_sub_i32 s21, s24, 16
	s_bitcmp0_b32 s21, 2
	s_cselect_b32 s21, 1, 0
	s_cmp_lt_u32 s24, 40
	s_cselect_b32 s21, s21, 0
	s_or_b32 s20, s20, s21
	s_cmp_lg_u32 s20, 0
	s_cselect_b64 s[20:21], -1, 0
	v_cndmask_b32_e64 v91, v83, v87, s[20:21]
	v_cndmask_b32_e64 v92, v84, v88, s[20:21]
	v_cndmask_b32_e64 v93, v85, v89, s[20:21]
	v_cndmask_b32_e64 v94, v86, v90, s[20:21]
	ds_read_b32 v226, v113
	ds_read_b32 v227, v113 offset:512
	ds_read_b32 v228, v113 offset:1024
	ds_read_b32 v229, v113 offset:1536
	ds_read_b32 v230, v113 offset:2048
	ds_read_b32 v231, v113 offset:2560
	ds_read_b32 v232, v113 offset:3072
	ds_read_b32 v233, v113 offset:3584
	s_waitcnt lgkmcnt(0)
	v_bfe_u32 v120, v226, 16, 1
	v_bfe_u32 v121, v227, 16, 1
	v_bfe_u32 v122, v228, 16, 1
	v_bfe_u32 v123, v229, 16, 1
	v_bfe_u32 v124, v230, 16, 1
	v_bfe_u32 v125, v231, 16, 1
	v_bfe_u32 v126, v232, 16, 1
	v_bfe_u32 v127, v233, 16, 1
	v_add3_u32 v226, v226, v120, s63
	v_add3_u32 v227, v227, v121, s63
	v_add3_u32 v228, v228, v122, s63
	v_add3_u32 v229, v229, v123, s63
	v_add3_u32 v230, v230, v124, s63
	v_add3_u32 v231, v231, v125, s63
	v_add3_u32 v232, v232, v126, s63
	v_add3_u32 v233, v233, v127, s63
	v_perm_b32 v242, v227, v226, s64
	v_perm_b32 v243, v229, v228, s64
	v_perm_b32 v244, v231, v230, s64
	v_perm_b32 v245, v233, v232, s64
	s_nop 0
	global_store_dwordx4 v91, v[242:245], s[6:7]
	ds_read_b32 v226, v115
	ds_read_b32 v227, v115 offset:512
	ds_read_b32 v228, v115 offset:1024
	ds_read_b32 v229, v115 offset:1536
	ds_read_b32 v230, v115 offset:2048
	ds_read_b32 v231, v115 offset:2560
	ds_read_b32 v232, v115 offset:3072
	ds_read_b32 v233, v115 offset:3584
	s_waitcnt lgkmcnt(0)
	v_bfe_u32 v120, v226, 16, 1
	v_bfe_u32 v121, v227, 16, 1
	v_bfe_u32 v122, v228, 16, 1
	v_bfe_u32 v123, v229, 16, 1
	v_bfe_u32 v124, v230, 16, 1
	v_bfe_u32 v125, v231, 16, 1
	v_bfe_u32 v126, v232, 16, 1
	v_bfe_u32 v127, v233, 16, 1
	v_add3_u32 v226, v226, v120, s63
	v_add3_u32 v227, v227, v121, s63
	v_add3_u32 v228, v228, v122, s63
	v_add3_u32 v229, v229, v123, s63
	v_add3_u32 v230, v230, v124, s63
	v_add3_u32 v231, v231, v125, s63
	v_add3_u32 v232, v232, v126, s63
	v_add3_u32 v233, v233, v127, s63
	v_perm_b32 v242, v227, v226, s64
	v_perm_b32 v243, v229, v228, s64
	v_perm_b32 v244, v231, v230, s64
	v_perm_b32 v245, v233, v232, s64
	s_nop 0
	global_store_dwordx4 v92, v[242:245], s[6:7]
	ds_read_b32 v226, v117
	ds_read_b32 v227, v117 offset:512
	ds_read_b32 v228, v117 offset:1024
	ds_read_b32 v229, v117 offset:1536
	ds_read_b32 v230, v117 offset:2048
	ds_read_b32 v231, v117 offset:2560
	ds_read_b32 v232, v117 offset:3072
	ds_read_b32 v233, v117 offset:3584
	s_waitcnt lgkmcnt(0)
	v_bfe_u32 v120, v226, 16, 1
	v_bfe_u32 v121, v227, 16, 1
	v_bfe_u32 v122, v228, 16, 1
	v_bfe_u32 v123, v229, 16, 1
	v_bfe_u32 v124, v230, 16, 1
	v_bfe_u32 v125, v231, 16, 1
	v_bfe_u32 v126, v232, 16, 1
	v_bfe_u32 v127, v233, 16, 1
	v_add3_u32 v226, v226, v120, s63
	v_add3_u32 v227, v227, v121, s63
	v_add3_u32 v228, v228, v122, s63
	v_add3_u32 v229, v229, v123, s63
	v_add3_u32 v230, v230, v124, s63
	v_add3_u32 v231, v231, v125, s63
	v_add3_u32 v232, v232, v126, s63
	v_add3_u32 v233, v233, v127, s63
	v_perm_b32 v242, v227, v226, s64
	v_perm_b32 v243, v229, v228, s64
	v_perm_b32 v244, v231, v230, s64
	v_perm_b32 v245, v233, v232, s64
	s_nop 0
	global_store_dwordx4 v93, v[242:245], s[6:7]
	ds_read_b32 v226, v119
	ds_read_b32 v227, v119 offset:512
	ds_read_b32 v228, v119 offset:1024
	ds_read_b32 v229, v119 offset:1536
	ds_read_b32 v230, v119 offset:2048
	ds_read_b32 v231, v119 offset:2560
	ds_read_b32 v232, v119 offset:3072
	ds_read_b32 v233, v119 offset:3584
	s_waitcnt lgkmcnt(0)
	v_bfe_u32 v120, v226, 16, 1
	v_bfe_u32 v121, v227, 16, 1
	v_bfe_u32 v122, v228, 16, 1
	v_bfe_u32 v123, v229, 16, 1
	v_bfe_u32 v124, v230, 16, 1
	v_bfe_u32 v125, v231, 16, 1
	v_bfe_u32 v126, v232, 16, 1
	v_bfe_u32 v127, v233, 16, 1
	v_add3_u32 v226, v226, v120, s63
	v_add3_u32 v227, v227, v121, s63
	v_add3_u32 v228, v228, v122, s63
	v_add3_u32 v229, v229, v123, s63
	v_add3_u32 v230, v230, v124, s63
	v_add3_u32 v231, v231, v125, s63
	v_add3_u32 v232, v232, v126, s63
	v_add3_u32 v233, v233, v127, s63
	v_perm_b32 v242, v227, v226, s64
	v_perm_b32 v243, v229, v228, s64
	v_perm_b32 v244, v231, v230, s64
	v_perm_b32 v245, v233, v232, s64
	s_nop 0
	global_store_dwordx4 v94, v[242:245], s[6:7]
	s_waitcnt vmcnt(16)
	v_mul_f32_e32 v144, v42, v144
	v_mul_f32_e32 v145, v42, v145
	v_mul_f32_e32 v146, v42, v146
	v_mul_f32_e32 v147, v42, v147
	ds_write_b128 v209, v[144:147]
	v_mul_f32_e32 v148, v43, v148
	v_mul_f32_e32 v149, v43, v149
	v_mul_f32_e32 v150, v43, v150
	v_mul_f32_e32 v151, v43, v151
	ds_write_b128 v209, v[148:151] offset:1024
	v_mul_f32_e32 v152, v44, v152
	v_mul_f32_e32 v153, v44, v153
	v_mul_f32_e32 v154, v44, v154
	v_mul_f32_e32 v155, v44, v155
	ds_write_b128 v209, v[152:155] offset:2048
	v_mul_f32_e32 v156, v45, v156
	v_mul_f32_e32 v157, v45, v157
	v_mul_f32_e32 v158, v45, v158
	v_mul_f32_e32 v159, v45, v159
	ds_write_b128 v209, v[156:159] offset:3072
	v_mul_f32_e32 v160, v46, v160
	v_mul_f32_e32 v161, v46, v161
	v_mul_f32_e32 v162, v46, v162
	v_mul_f32_e32 v163, v46, v163
	ds_write_b128 v209, v[160:163] offset:4096
	v_mul_f32_e32 v164, v47, v164
	v_mul_f32_e32 v165, v47, v165
	v_mul_f32_e32 v166, v47, v166
	v_mul_f32_e32 v167, v47, v167
	ds_write_b128 v209, v[164:167] offset:5120
	v_mul_f32_e32 v168, v48, v168
	v_mul_f32_e32 v169, v48, v169
	v_mul_f32_e32 v170, v48, v170
	v_mul_f32_e32 v171, v48, v171
	ds_write_b128 v209, v[168:171] offset:6144
	v_mul_f32_e32 v172, v49, v172
	v_mul_f32_e32 v173, v49, v173
	v_mul_f32_e32 v174, v49, v174
	v_mul_f32_e32 v175, v49, v175
	ds_write_b128 v209, v[172:175] offset:7168
	s_waitcnt lgkmcnt(0)
	s_barrier
; #define GAS __attribute__((address_space(1)))
; #define LAS __attribute__((address_space(3)))
; #define LDS_WAIT() asm volatile("s_waitcnt lgkmcnt(0)" ::: "memory")
; __device__ __forceinline__ unsigned pk2(float lo, float hi) { return f2bf(lo) | (f2bf(hi) << 16); }
; __device__ __forceinline__ int nat_dim(int p) { return (p >> 1) + 64 * (p & 1); }
; __device__ __forceinline__ int src_col_in(int c) {
;     if (c < 5120) { const int blk = c >> 7, p = c & 127; const bool rope = blk < 16 || ((((blk - 16) >> 2) & 1) == 0); const int d = rope ? (p >> 1) + 64 * (p & 1) : p; return blk * 128 + d; }
;     if (c < OFF_Z) return c + 2096;
;     if (c < OFF_G) return c - 4048;
;     if (c < OFF_DT) return 5120 + (c - OFF_G);
;     if (c < NSRC) return c;
;     return -1;
; }
; template <int MAP, bool KS, bool KPERM = false>
; __device__ __forceinline__ void p0_transpose_item(const float* W, int K, int Nsrc, int nblk, bf16* WT, const float* ksA, const float* ksB, int ksplit, LAS float* scr, int item, int lane) {
;     const int kb = item / nblk, nb = item % nblk, k0 = 64 * kb, n0 = 32 * nb;
;     const int nr = n0 + (lane & 31); const int sc = MAP == 1 ? src_col_in(nr) : (MAP == 2 ? nat_dim(nr) : nr);
;     float v[32];
; #pragma unroll
;     for (int i = 0; i < 32; ++i) { const int k = k0 + 2 * i + (lane >> 5); const int ksrc = KPERM ? ((k & ~127) + nat_dim(k & 127)) : k;
;         v[i] = sc >= 0 ? W[(size_t)ksrc * Nsrc + sc] : 0.f; }
; #pragma unroll
;     for (int i = 0; i < 32; ++i) { const int kk = 2 * i + (lane >> 5); const int k = k0 + kk;
;         if (KS) v[i] *= (k < ksplit ? ksA[k] : ksB[k - ksplit]);
;         scr[kk * 33 + (lane & 31)] = v[i]; }
;     LDS_WAIT(); asm volatile("" ::: "memory");
;     const int c = lane & 7;
; #pragma unroll
;     for (int j = 0; j < 4; ++j) { const int n = (lane >> 3) + 8 * j; const LAS float* s = scr + (8 * c) * 33 + n;
;         v4u o; o.x = pk2(s[0 * 33], s[1 * 33]); o.y = pk2(s[2 * 33], s[3 * 33]); o.z = pk2(s[4 * 33], s[5 * 33]); o.w = pk2(s[6 * 33], s[7 * 33]);
;         *(GAS v4u*)(WT + (size_t)(n0 + n) * K + k0 + 8 * c) = o; }
;     LDS_WAIT(); asm volatile("" ::: "memory");
; }
	s_add_i32 s24, s23, 48
	s_lshl_b32 s20, s24, 7
	s_cmp_lt_u32 s24, 40
	s_cselect_b32 s21, 0, 0x830
	s_cmp_lt_u32 s24, 72
	s_cselect_b32 s21, s21, 0xfffff030
	s_add_i32 s20, s20, s21
	s_lshl_b32 s20, s20, 2
	s_add_u32 s8, s46, s20
	s_addc_u32 s9, s47, 0
	global_load_dwordx4 v[144:147], v76, s[8:9]
	s_add_u32 s8, s8, 0x16280
	s_addc_u32 s9, s9, 0
	global_load_dwordx4 v[148:151], v76, s[8:9]
	s_add_u32 s8, s8, 0x16280
	s_addc_u32 s9, s9, 0
	global_load_dwordx4 v[152:155], v76, s[8:9]
	s_add_u32 s8, s8, 0x16280
	s_addc_u32 s9, s9, 0
	global_load_dwordx4 v[156:159], v76, s[8:9]
	s_add_u32 s8, s8, 0x16280
	s_addc_u32 s9, s9, 0
	global_load_dwordx4 v[160:163], v76, s[8:9]
	s_add_u32 s8, s8, 0x16280
	s_addc_u32 s9, s9, 0
	global_load_dwordx4 v[164:167], v76, s[8:9]
	s_add_u32 s8, s8, 0x16280
	s_addc_u32 s9, s9, 0
	global_load_dwordx4 v[168:171], v76, s[8:9]
	s_add_u32 s8, s8, 0x16280
	s_addc_u32 s9, s9, 0
	global_load_dwordx4 v[172:175], v76, s[8:9]
	s_add_i32 s24, s23, 32
	s_mul_i32 s20, s24, 0x100000
	s_add_u32 s6, s48, s20
	s_addc_u32 s7, s49, 0
	s_cmp_lt_u32 s24, 16
	s_cselect_b32 s20, 1, 0
	s_sub_i32 s21, s24, 16
	s_bitcmp0_b32 s21, 2
	s_cselect_b32 s21, 1, 0
	s_cmp_lt_u32 s24, 40
	s_cselect_b32 s21, s21, 0
	s_or_b32 s20, s20, s21
	s_cmp_lg_u32 s20, 0
	s_cselect_b64 s[20:21], -1, 0
	v_cndmask_b32_e64 v91, v83, v87, s[20:21]
	v_cndmask_b32_e64 v92, v84, v88, s[20:21]
	v_cndmask_b32_e64 v93, v85, v89, s[20:21]
	v_cndmask_b32_e64 v94, v86, v90, s[20:21]
	ds_read_b32 v226, v112
	ds_read_b32 v227, v112 offset:512
	ds_read_b32 v228, v112 offset:1024
	ds_read_b32 v229, v112 offset:1536
	ds_read_b32 v230, v112 offset:2048
	ds_read_b32 v231, v112 offset:2560
	ds_read_b32 v232, v112 offset:3072
	ds_read_b32 v233, v112 offset:3584
	s_waitcnt lgkmcnt(0)
	v_bfe_u32 v120, v226, 16, 1
	v_bfe_u32 v121, v227, 16, 1
	v_bfe_u32 v122, v228, 16, 1
	v_bfe_u32 v123, v229, 16, 1
	v_bfe_u32 v124, v230, 16, 1
	v_bfe_u32 v125, v231, 16, 1
	v_bfe_u32 v126, v232, 16, 1
	v_bfe_u32 v127, v233, 16, 1
	v_add3_u32 v226, v226, v120, s63
	v_add3_u32 v227, v227, v121, s63
	v_add3_u32 v228, v228, v122, s63
	v_add3_u32 v229, v229, v123, s63
	v_add3_u32 v230, v230, v124, s63
	v_add3_u32 v231, v231, v125, s63
	v_add3_u32 v232, v232, v126, s63
	v_add3_u32 v233, v233, v127, s63
	v_perm_b32 v242, v227, v226, s64
	v_perm_b32 v243, v229, v228, s64
	v_perm_b32 v244, v231, v230, s64
	v_perm_b32 v245, v233, v232, s64
	s_nop 0
	global_store_dwordx4 v91, v[242:245], s[6:7]
	ds_read_b32 v226, v114
	ds_read_b32 v227, v114 offset:512
	ds_read_b32 v228, v114 offset:1024
	ds_read_b32 v229, v114 offset:1536
	ds_read_b32 v230, v114 offset:2048
	ds_read_b32 v231, v114 offset:2560
	ds_read_b32 v232, v114 offset:3072
	ds_read_b32 v233, v114 offset:3584
	s_waitcnt lgkmcnt(0)
	v_bfe_u32 v120, v226, 16, 1
	v_bfe_u32 v121, v227, 16, 1
	v_bfe_u32 v122, v228, 16, 1
	v_bfe_u32 v123, v229, 16, 1
	v_bfe_u32 v124, v230, 16, 1
	v_bfe_u32 v125, v231, 16, 1
	v_bfe_u32 v126, v232, 16, 1
	v_bfe_u32 v127, v233, 16, 1
	v_add3_u32 v226, v226, v120, s63
	v_add3_u32 v227, v227, v121, s63
	v_add3_u32 v228, v228, v122, s63
	v_add3_u32 v229, v229, v123, s63
	v_add3_u32 v230, v230, v124, s63
	v_add3_u32 v231, v231, v125, s63
	v_add3_u32 v232, v232, v126, s63
	v_add3_u32 v233, v233, v127, s63
	v_perm_b32 v242, v227, v226, s64
	v_perm_b32 v243, v229, v228, s64
	v_perm_b32 v244, v231, v230, s64
	v_perm_b32 v245, v233, v232, s64
	s_nop 0
	global_store_dwordx4 v92, v[242:245], s[6:7]
	ds_read_b32 v226, v116
	ds_read_b32 v227, v116 offset:512
	ds_read_b32 v228, v116 offset:1024
	ds_read_b32 v229, v116 offset:1536
	ds_read_b32 v230, v116 offset:2048
	ds_read_b32 v231, v116 offset:2560
	ds_read_b32 v232, v116 offset:3072
	ds_read_b32 v233, v116 offset:3584
	s_waitcnt lgkmcnt(0)
	v_bfe_u32 v120, v226, 16, 1
	v_bfe_u32 v121, v227, 16, 1
	v_bfe_u32 v122, v228, 16, 1
	v_bfe_u32 v123, v229, 16, 1
	v_bfe_u32 v124, v230, 16, 1
	v_bfe_u32 v125, v231, 16, 1
	v_bfe_u32 v126, v232, 16, 1
	v_bfe_u32 v127, v233, 16, 1
	v_add3_u32 v226, v226, v120, s63
	v_add3_u32 v227, v227, v121, s63
	v_add3_u32 v228, v228, v122, s63
	v_add3_u32 v229, v229, v123, s63
	v_add3_u32 v230, v230, v124, s63
	v_add3_u32 v231, v231, v125, s63
	v_add3_u32 v232, v232, v126, s63
	v_add3_u32 v233, v233, v127, s63
	v_perm_b32 v242, v227, v226, s64
	v_perm_b32 v243, v229, v228, s64
	v_perm_b32 v244, v231, v230, s64
	v_perm_b32 v245, v233, v232, s64
	s_nop 0
	global_store_dwordx4 v93, v[242:245], s[6:7]
	ds_read_b32 v226, v118
	ds_read_b32 v227, v118 offset:512
	ds_read_b32 v228, v118 offset:1024
	ds_read_b32 v229, v118 offset:1536
	ds_read_b32 v230, v118 offset:2048
	ds_read_b32 v231, v118 offset:2560
	ds_read_b32 v232, v118 offset:3072
	ds_read_b32 v233, v118 offset:3584
	s_waitcnt lgkmcnt(0)
	v_bfe_u32 v120, v226, 16, 1
	v_bfe_u32 v121, v227, 16, 1
	v_bfe_u32 v122, v228, 16, 1
	v_bfe_u32 v123, v229, 16, 1
	v_bfe_u32 v124, v230, 16, 1
	v_bfe_u32 v125, v231, 16, 1
	v_bfe_u32 v126, v232, 16, 1
	v_bfe_u32 v127, v233, 16, 1
	v_add3_u32 v226, v226, v120, s63
	v_add3_u32 v227, v227, v121, s63
	v_add3_u32 v228, v228, v122, s63
	v_add3_u32 v229, v229, v123, s63
	v_add3_u32 v230, v230, v124, s63
	v_add3_u32 v231, v231, v125, s63
	v_add3_u32 v232, v232, v126, s63
	v_add3_u32 v233, v233, v127, s63
	v_perm_b32 v242, v227, v226, s64
	v_perm_b32 v243, v229, v228, s64
	v_perm_b32 v244, v231, v230, s64
	v_perm_b32 v245, v233, v232, s64
	s_nop 0
	global_store_dwordx4 v94, v[242:245], s[6:7]
	s_waitcnt vmcnt(16)
	v_mul_f32_e32 v176, v42, v176
	v_mul_f32_e32 v177, v42, v177
	v_mul_f32_e32 v178, v42, v178
	v_mul_f32_e32 v179, v42, v179
	ds_write_b128 v210, v[176:179]
	v_mul_f32_e32 v180, v43, v180
	v_mul_f32_e32 v181, v43, v181
	v_mul_f32_e32 v182, v43, v182
	v_mul_f32_e32 v183, v43, v183
	ds_write_b128 v210, v[180:183] offset:1024
	v_mul_f32_e32 v184, v44, v184
	v_mul_f32_e32 v185, v44, v185
	v_mul_f32_e32 v186, v44, v186
	v_mul_f32_e32 v187, v44, v187
	ds_write_b128 v210, v[184:187] offset:2048
	v_mul_f32_e32 v188, v45, v188
	v_mul_f32_e32 v189, v45, v189
	v_mul_f32_e32 v190, v45, v190
	v_mul_f32_e32 v191, v45, v191
	ds_write_b128 v210, v[188:191] offset:3072
	v_mul_f32_e32 v192, v46, v192
	v_mul_f32_e32 v193, v46, v193
	v_mul_f32_e32 v194, v46, v194
	v_mul_f32_e32 v195, v46, v195
	ds_write_b128 v210, v[192:195] offset:4096
	v_mul_f32_e32 v196, v47, v196
	v_mul_f32_e32 v197, v47, v197
	v_mul_f32_e32 v198, v47, v198
	v_mul_f32_e32 v199, v47, v199
	ds_write_b128 v210, v[196:199] offset:5120
	v_mul_f32_e32 v200, v48, v200
	v_mul_f32_e32 v201, v48, v201
	v_mul_f32_e32 v202, v48, v202
	v_mul_f32_e32 v203, v48, v203
	ds_write_b128 v210, v[200:203] offset:6144
	v_mul_f32_e32 v204, v49, v204
	v_mul_f32_e32 v205, v49, v205
	v_mul_f32_e32 v206, v49, v206
	v_mul_f32_e32 v207, v49, v207
	ds_write_b128 v210, v[204:207] offset:7168
	s_waitcnt lgkmcnt(0)
	s_barrier
; #define GAS __attribute__((address_space(1)))
; #define LAS __attribute__((address_space(3)))
; #define LDS_WAIT() asm volatile("s_waitcnt lgkmcnt(0)" ::: "memory")
; __device__ __forceinline__ unsigned pk2(float lo, float hi) { return f2bf(lo) | (f2bf(hi) << 16); }
; __device__ __forceinline__ int nat_dim(int p) { return (p >> 1) + 64 * (p & 1); }
; __device__ __forceinline__ int src_col_in(int c) {
;     if (c < 5120) { const int blk = c >> 7, p = c & 127; const bool rope = blk < 16 || ((((blk - 16) >> 2) & 1) == 0); const int d = rope ? (p >> 1) + 64 * (p & 1) : p; return blk * 128 + d; }
;     if (c < OFF_Z) return c + 2096;
;     if (c < OFF_G) return c - 4048;
;     if (c < OFF_DT) return 5120 + (c - OFF_G);
;     if (c < NSRC) return c;
;     return -1;
; }
; template <int MAP, bool KS, bool KPERM = false>
; __device__ __forceinline__ void p0_transpose_item(const float* W, int K, int Nsrc, int nblk, bf16* WT, const float* ksA, const float* ksB, int ksplit, LAS float* scr, int item, int lane) {
;     const int kb = item / nblk, nb = item % nblk, k0 = 64 * kb, n0 = 32 * nb;
;     const int nr = n0 + (lane & 31); const int sc = MAP == 1 ? src_col_in(nr) : (MAP == 2 ? nat_dim(nr) : nr);
;     float v[32];
; #pragma unroll
;     for (int i = 0; i < 32; ++i) { const int k = k0 + 2 * i + (lane >> 5); const int ksrc = KPERM ? ((k & ~127) + nat_dim(k & 127)) : k;
;         v[i] = sc >= 0 ? W[(size_t)ksrc * Nsrc + sc] : 0.f; }
; #pragma unroll
;     for (int i = 0; i < 32; ++i) { const int kk = 2 * i + (lane >> 5); const int k = k0 + kk;
;         if (KS) v[i] *= (k < ksplit ? ksA[k] : ksB[k - ksplit]);
;         scr[kk * 33 + (lane & 31)] = v[i]; }
;     LDS_WAIT(); asm volatile("" ::: "memory");
;     const int c = lane & 7;
; #pragma unroll
;     for (int j = 0; j < 4; ++j) { const int n = (lane >> 3) + 8 * j; const LAS float* s = scr + (8 * c) * 33 + n;
;         v4u o; o.x = pk2(s[0 * 33], s[1 * 33]); o.y = pk2(s[2 * 33], s[3 * 33]); o.z = pk2(s[4 * 33], s[5 * 33]); o.w = pk2(s[6 * 33], s[7 * 33]);
;         *(GAS v4u*)(WT + (size_t)(n0 + n) * K + k0 + 8 * c) = o; }
;     LDS_WAIT(); asm volatile("" ::: "memory");
; }
	s_add_i32 s24, s23, 56
	s_lshl_b32 s20, s24, 7
	s_cmp_lt_u32 s24, 40
	s_cselect_b32 s21, 0, 0x830
	s_cmp_lt_u32 s24, 72
	s_cselect_b32 s21, s21, 0xfffff030
	s_add_i32 s20, s20, s21
	s_lshl_b32 s20, s20, 2
	s_add_u32 s8, s46, s20
	s_addc_u32 s9, s47, 0
	global_load_dwordx4 v[176:179], v76, s[8:9]
	s_add_u32 s8, s8, 0x16280
	s_addc_u32 s9, s9, 0
	global_load_dwordx4 v[180:183], v76, s[8:9]
	s_add_u32 s8, s8, 0x16280
	s_addc_u32 s9, s9, 0
	global_load_dwordx4 v[184:187], v76, s[8:9]
	s_add_u32 s8, s8, 0x16280
	s_addc_u32 s9, s9, 0
	global_load_dwordx4 v[188:191], v76, s[8:9]
	s_add_u32 s8, s8, 0x16280
	s_addc_u32 s9, s9, 0
	global_load_dwordx4 v[192:195], v76, s[8:9]
	s_add_u32 s8, s8, 0x16280
	s_addc_u32 s9, s9, 0
	global_load_dwordx4 v[196:199], v76, s[8:9]
	s_add_u32 s8, s8, 0x16280
	s_addc_u32 s9, s9, 0
	global_load_dwordx4 v[200:203], v76, s[8:9]
	s_add_u32 s8, s8, 0x16280
	s_addc_u32 s9, s9, 0
	global_load_dwordx4 v[204:207], v76, s[8:9]
	s_add_i32 s24, s23, 40
	s_mul_i32 s20, s24, 0x100000
	s_add_u32 s6, s48, s20
	s_addc_u32 s7, s49, 0
	s_cmp_lt_u32 s24, 16
	s_cselect_b32 s20, 1, 0
	s_sub_i32 s21, s24, 16
	s_bitcmp0_b32 s21, 2
	s_cselect_b32 s21, 1, 0
	s_cmp_lt_u32 s24, 40
	s_cselect_b32 s21, s21, 0
	s_or_b32 s20, s20, s21
	s_cmp_lg_u32 s20, 0
	s_cselect_b64 s[20:21], -1, 0
	v_cndmask_b32_e64 v91, v83, v87, s[20:21]
	v_cndmask_b32_e64 v92, v84, v88, s[20:21]
	v_cndmask_b32_e64 v93, v85, v89, s[20:21]
	v_cndmask_b32_e64 v94, v86, v90, s[20:21]
	ds_read_b32 v226, v113
	ds_read_b32 v227, v113 offset:512
	ds_read_b32 v228, v113 offset:1024
	ds_read_b32 v229, v113 offset:1536
	ds_read_b32 v230, v113 offset:2048
	ds_read_b32 v231, v113 offset:2560
	ds_read_b32 v232, v113 offset:3072
	ds_read_b32 v233, v113 offset:3584
	s_waitcnt lgkmcnt(0)
	v_bfe_u32 v120, v226, 16, 1
	v_bfe_u32 v121, v227, 16, 1
	v_bfe_u32 v122, v228, 16, 1
	v_bfe_u32 v123, v229, 16, 1
	v_bfe_u32 v124, v230, 16, 1
	v_bfe_u32 v125, v231, 16, 1
	v_bfe_u32 v126, v232, 16, 1
	v_bfe_u32 v127, v233, 16, 1
	v_add3_u32 v226, v226, v120, s63
	v_add3_u32 v227, v227, v121, s63
	v_add3_u32 v228, v228, v122, s63
	v_add3_u32 v229, v229, v123, s63
	v_add3_u32 v230, v230, v124, s63
	v_add3_u32 v231, v231, v125, s63
	v_add3_u32 v232, v232, v126, s63
	v_add3_u32 v233, v233, v127, s63
	v_perm_b32 v242, v227, v226, s64
	v_perm_b32 v243, v229, v228, s64
	v_perm_b32 v244, v231, v230, s64
	v_perm_b32 v245, v233, v232, s64
	s_nop 0
	global_store_dwordx4 v91, v[242:245], s[6:7]
	ds_read_b32 v226, v115
	ds_read_b32 v227, v115 offset:512
	ds_read_b32 v228, v115 offset:1024
	ds_read_b32 v229, v115 offset:1536
	ds_read_b32 v230, v115 offset:2048
	ds_read_b32 v231, v115 offset:2560
	ds_read_b32 v232, v115 offset:3072
	ds_read_b32 v233, v115 offset:3584
	s_waitcnt lgkmcnt(0)
	v_bfe_u32 v120, v226, 16, 1
	v_bfe_u32 v121, v227, 16, 1
	v_bfe_u32 v122, v228, 16, 1
	v_bfe_u32 v123, v229, 16, 1
	v_bfe_u32 v124, v230, 16, 1
	v_bfe_u32 v125, v231, 16, 1
	v_bfe_u32 v126, v232, 16, 1
	v_bfe_u32 v127, v233, 16, 1
	v_add3_u32 v226, v226, v120, s63
	v_add3_u32 v227, v227, v121, s63
	v_add3_u32 v228, v228, v122, s63
	v_add3_u32 v229, v229, v123, s63
	v_add3_u32 v230, v230, v124, s63
	v_add3_u32 v231, v231, v125, s63
	v_add3_u32 v232, v232, v126, s63
	v_add3_u32 v233, v233, v127, s63
	v_perm_b32 v242, v227, v226, s64
	v_perm_b32 v243, v229, v228, s64
	v_perm_b32 v244, v231, v230, s64
	v_perm_b32 v245, v233, v232, s64
	s_nop 0
	global_store_dwordx4 v92, v[242:245], s[6:7]
	ds_read_b32 v226, v117
	ds_read_b32 v227, v117 offset:512
	ds_read_b32 v228, v117 offset:1024
	ds_read_b32 v229, v117 offset:1536
	ds_read_b32 v230, v117 offset:2048
	ds_read_b32 v231, v117 offset:2560
	ds_read_b32 v232, v117 offset:3072
	ds_read_b32 v233, v117 offset:3584
	s_waitcnt lgkmcnt(0)
	v_bfe_u32 v120, v226, 16, 1
	v_bfe_u32 v121, v227, 16, 1
	v_bfe_u32 v122, v228, 16, 1
	v_bfe_u32 v123, v229, 16, 1
	v_bfe_u32 v124, v230, 16, 1
	v_bfe_u32 v125, v231, 16, 1
	v_bfe_u32 v126, v232, 16, 1
	v_bfe_u32 v127, v233, 16, 1
	v_add3_u32 v226, v226, v120, s63
	v_add3_u32 v227, v227, v121, s63
	v_add3_u32 v228, v228, v122, s63
	v_add3_u32 v229, v229, v123, s63
	v_add3_u32 v230, v230, v124, s63
	v_add3_u32 v231, v231, v125, s63
	v_add3_u32 v232, v232, v126, s63
	v_add3_u32 v233, v233, v127, s63
	v_perm_b32 v242, v227, v226, s64
	v_perm_b32 v243, v229, v228, s64
	v_perm_b32 v244, v231, v230, s64
	v_perm_b32 v245, v233, v232, s64
	s_nop 0
	global_store_dwordx4 v93, v[242:245], s[6:7]
	ds_read_b32 v226, v119
	ds_read_b32 v227, v119 offset:512
	ds_read_b32 v228, v119 offset:1024
	ds_read_b32 v229, v119 offset:1536
	ds_read_b32 v230, v119 offset:2048
	ds_read_b32 v231, v119 offset:2560
	ds_read_b32 v232, v119 offset:3072
	ds_read_b32 v233, v119 offset:3584
	s_waitcnt lgkmcnt(0)
	v_bfe_u32 v120, v226, 16, 1
	v_bfe_u32 v121, v227, 16, 1
	v_bfe_u32 v122, v228, 16, 1
	v_bfe_u32 v123, v229, 16, 1
	v_bfe_u32 v124, v230, 16, 1
	v_bfe_u32 v125, v231, 16, 1
	v_bfe_u32 v126, v232, 16, 1
	v_bfe_u32 v127, v233, 16, 1
	v_add3_u32 v226, v226, v120, s63
	v_add3_u32 v227, v227, v121, s63
	v_add3_u32 v228, v228, v122, s63
	v_add3_u32 v229, v229, v123, s63
	v_add3_u32 v230, v230, v124, s63
	v_add3_u32 v231, v231, v125, s63
	v_add3_u32 v232, v232, v126, s63
	v_add3_u32 v233, v233, v127, s63
	v_perm_b32 v242, v227, v226, s64
	v_perm_b32 v243, v229, v228, s64
	v_perm_b32 v244, v231, v230, s64
	v_perm_b32 v245, v233, v232, s64
	s_nop 0
	global_store_dwordx4 v94, v[242:245], s[6:7]
	s_waitcnt vmcnt(16)
	v_mul_f32_e32 v144, v42, v144
	v_mul_f32_e32 v145, v42, v145
	v_mul_f32_e32 v146, v42, v146
	v_mul_f32_e32 v147, v42, v147
	ds_write_b128 v209, v[144:147]
	v_mul_f32_e32 v148, v43, v148
	v_mul_f32_e32 v149, v43, v149
	v_mul_f32_e32 v150, v43, v150
	v_mul_f32_e32 v151, v43, v151
	ds_write_b128 v209, v[148:151] offset:1024
	v_mul_f32_e32 v152, v44, v152
	v_mul_f32_e32 v153, v44, v153
	v_mul_f32_e32 v154, v44, v154
	v_mul_f32_e32 v155, v44, v155
	ds_write_b128 v209, v[152:155] offset:2048
	v_mul_f32_e32 v156, v45, v156
	v_mul_f32_e32 v157, v45, v157
	v_mul_f32_e32 v158, v45, v158
	v_mul_f32_e32 v159, v45, v159
	ds_write_b128 v209, v[156:159] offset:3072
	v_mul_f32_e32 v160, v46, v160
	v_mul_f32_e32 v161, v46, v161
	v_mul_f32_e32 v162, v46, v162
	v_mul_f32_e32 v163, v46, v163
	ds_write_b128 v209, v[160:163] offset:4096
	v_mul_f32_e32 v164, v47, v164
	v_mul_f32_e32 v165, v47, v165
	v_mul_f32_e32 v166, v47, v166
	v_mul_f32_e32 v167, v47, v167
	ds_write_b128 v209, v[164:167] offset:5120
	v_mul_f32_e32 v168, v48, v168
	v_mul_f32_e32 v169, v48, v169
	v_mul_f32_e32 v170, v48, v170
	v_mul_f32_e32 v171, v48, v171
	ds_write_b128 v209, v[168:171] offset:6144
	v_mul_f32_e32 v172, v49, v172
	v_mul_f32_e32 v173, v49, v173
	v_mul_f32_e32 v174, v49, v174
	v_mul_f32_e32 v175, v49, v175
	ds_write_b128 v209, v[172:175] offset:7168
	s_waitcnt lgkmcnt(0)
	s_barrier
; #define GAS __attribute__((address_space(1)))
; #define LAS __attribute__((address_space(3)))
; #define LDS_WAIT() asm volatile("s_waitcnt lgkmcnt(0)" ::: "memory")
; __device__ __forceinline__ unsigned pk2(float lo, float hi) { return f2bf(lo) | (f2bf(hi) << 16); }
; __device__ __forceinline__ int nat_dim(int p) { return (p >> 1) + 64 * (p & 1); }
; __device__ __forceinline__ int src_col_in(int c) {
;     if (c < 5120) { const int blk = c >> 7, p = c & 127; const bool rope = blk < 16 || ((((blk - 16) >> 2) & 1) == 0); const int d = rope ? (p >> 1) + 64 * (p & 1) : p; return blk * 128 + d; }
;     if (c < OFF_Z) return c + 2096;
;     if (c < OFF_G) return c - 4048;
;     if (c < OFF_DT) return 5120 + (c - OFF_G);
;     if (c < NSRC) return c;
;     return -1;
; }
; template <int MAP, bool KS, bool KPERM = false>
; __device__ __forceinline__ void p0_transpose_item(const float* W, int K, int Nsrc, int nblk, bf16* WT, const float* ksA, const float* ksB, int ksplit, LAS float* scr, int item, int lane) {
;     const int kb = item / nblk, nb = item % nblk, k0 = 64 * kb, n0 = 32 * nb;
;     const int nr = n0 + (lane & 31); const int sc = MAP == 1 ? src_col_in(nr) : (MAP == 2 ? nat_dim(nr) : nr);
;     float v[32];
; #pragma unroll
;     for (int i = 0; i < 32; ++i) { const int k = k0 + 2 * i + (lane >> 5); const int ksrc = KPERM ? ((k & ~127) + nat_dim(k & 127)) : k;
;         v[i] = sc >= 0 ? W[(size_t)ksrc * Nsrc + sc] : 0.f; }
; #pragma unroll
;     for (int i = 0; i < 32; ++i) { const int kk = 2 * i + (lane >> 5); const int k = k0 + kk;
;         if (KS) v[i] *= (k < ksplit ? ksA[k] : ksB[k - ksplit]);
;         scr[kk * 33 + (lane & 31)] = v[i]; }
;     LDS_WAIT(); asm volatile("" ::: "memory");
;     const int c = lane & 7;
; #pragma unroll
;     for (int j = 0; j < 4; ++j) { const int n = (lane >> 3) + 8 * j; const LAS float* s = scr + (8 * c) * 33 + n;
;         v4u o; o.x = pk2(s[0 * 33], s[1 * 33]); o.y = pk2(s[2 * 33], s[3 * 33]); o.z = pk2(s[4 * 33], s[5 * 33]); o.w = pk2(s[6 * 33], s[7 * 33]);
;         *(GAS v4u*)(WT + (size_t)(n0 + n) * K + k0 + 8 * c) = o; }
;     LDS_WAIT(); asm volatile("" ::: "memory");
; }
	s_add_i32 s24, s23, 64
	s_lshl_b32 s20, s24, 7
	s_cmp_lt_u32 s24, 40
	s_cselect_b32 s21, 0, 0x830
	s_cmp_lt_u32 s24, 72
	s_cselect_b32 s21, s21, 0xfffff030
	s_add_i32 s20, s20, s21
	s_lshl_b32 s20, s20, 2
	s_add_u32 s8, s46, s20
	s_addc_u32 s9, s47, 0
	global_load_dwordx4 v[144:147], v76, s[8:9]
	s_add_u32 s8, s8, 0x16280
	s_addc_u32 s9, s9, 0
	global_load_dwordx4 v[148:151], v76, s[8:9]
	s_add_u32 s8, s8, 0x16280
	s_addc_u32 s9, s9, 0
	global_load_dwordx4 v[152:155], v76, s[8:9]
	s_add_u32 s8, s8, 0x16280
	s_addc_u32 s9, s9, 0
	global_load_dwordx4 v[156:159], v76, s[8:9]
	s_add_u32 s8, s8, 0x16280
	s_addc_u32 s9, s9, 0
	global_load_dwordx4 v[160:163], v76, s[8:9]
	s_add_u32 s8, s8, 0x16280
	s_addc_u32 s9, s9, 0
	global_load_dwordx4 v[164:167], v76, s[8:9]
	s_add_u32 s8, s8, 0x16280
	s_addc_u32 s9, s9, 0
	global_load_dwordx4 v[168:171], v76, s[8:9]
	s_add_u32 s8, s8, 0x16280
	s_addc_u32 s9, s9, 0
	global_load_dwordx4 v[172:175], v76, s[8:9]
	s_add_i32 s24, s23, 48
	s_mul_i32 s20, s24, 0x100000
	s_add_u32 s6, s48, s20
	s_addc_u32 s7, s49, 0
	s_cmp_lt_u32 s24, 16
	s_cselect_b32 s20, 1, 0
	s_sub_i32 s21, s24, 16
	s_bitcmp0_b32 s21, 2
	s_cselect_b32 s21, 1, 0
	s_cmp_lt_u32 s24, 40
	s_cselect_b32 s21, s21, 0
	s_or_b32 s20, s20, s21
	s_cmp_lg_u32 s20, 0
	s_cselect_b64 s[20:21], -1, 0
	v_cndmask_b32_e64 v91, v83, v87, s[20:21]
	v_cndmask_b32_e64 v92, v84, v88, s[20:21]
	v_cndmask_b32_e64 v93, v85, v89, s[20:21]
	v_cndmask_b32_e64 v94, v86, v90, s[20:21]
	ds_read_b32 v226, v112
	ds_read_b32 v227, v112 offset:512
	ds_read_b32 v228, v112 offset:1024
	ds_read_b32 v229, v112 offset:1536
	ds_read_b32 v230, v112 offset:2048
	ds_read_b32 v231, v112 offset:2560
	ds_read_b32 v232, v112 offset:3072
	ds_read_b32 v233, v112 offset:3584
	s_waitcnt lgkmcnt(0)
	v_bfe_u32 v120, v226, 16, 1
	v_bfe_u32 v121, v227, 16, 1
	v_bfe_u32 v122, v228, 16, 1
	v_bfe_u32 v123, v229, 16, 1
	v_bfe_u32 v124, v230, 16, 1
	v_bfe_u32 v125, v231, 16, 1
	v_bfe_u32 v126, v232, 16, 1
	v_bfe_u32 v127, v233, 16, 1
	v_add3_u32 v226, v226, v120, s63
	v_add3_u32 v227, v227, v121, s63
	v_add3_u32 v228, v228, v122, s63
	v_add3_u32 v229, v229, v123, s63
	v_add3_u32 v230, v230, v124, s63
	v_add3_u32 v231, v231, v125, s63
	v_add3_u32 v232, v232, v126, s63
	v_add3_u32 v233, v233, v127, s63
	v_perm_b32 v242, v227, v226, s64
	v_perm_b32 v243, v229, v228, s64
	v_perm_b32 v244, v231, v230, s64
	v_perm_b32 v245, v233, v232, s64
	s_nop 0
	global_store_dwordx4 v91, v[242:245], s[6:7]
	ds_read_b32 v226, v114
	ds_read_b32 v227, v114 offset:512
	ds_read_b32 v228, v114 offset:1024
	ds_read_b32 v229, v114 offset:1536
	ds_read_b32 v230, v114 offset:2048
	ds_read_b32 v231, v114 offset:2560
	ds_read_b32 v232, v114 offset:3072
	ds_read_b32 v233, v114 offset:3584
	s_waitcnt lgkmcnt(0)
	v_bfe_u32 v120, v226, 16, 1
	v_bfe_u32 v121, v227, 16, 1
	v_bfe_u32 v122, v228, 16, 1
	v_bfe_u32 v123, v229, 16, 1
	v_bfe_u32 v124, v230, 16, 1
	v_bfe_u32 v125, v231, 16, 1
	v_bfe_u32 v126, v232, 16, 1
	v_bfe_u32 v127, v233, 16, 1
	v_add3_u32 v226, v226, v120, s63
	v_add3_u32 v227, v227, v121, s63
	v_add3_u32 v228, v228, v122, s63
	v_add3_u32 v229, v229, v123, s63
	v_add3_u32 v230, v230, v124, s63
	v_add3_u32 v231, v231, v125, s63
	v_add3_u32 v232, v232, v126, s63
	v_add3_u32 v233, v233, v127, s63
	v_perm_b32 v242, v227, v226, s64
	v_perm_b32 v243, v229, v228, s64
	v_perm_b32 v244, v231, v230, s64
	v_perm_b32 v245, v233, v232, s64
	s_nop 0
	global_store_dwordx4 v92, v[242:245], s[6:7]
	ds_read_b32 v226, v116
	ds_read_b32 v227, v116 offset:512
	ds_read_b32 v228, v116 offset:1024
	ds_read_b32 v229, v116 offset:1536
	ds_read_b32 v230, v116 offset:2048
	ds_read_b32 v231, v116 offset:2560
	ds_read_b32 v232, v116 offset:3072
	ds_read_b32 v233, v116 offset:3584
	s_waitcnt lgkmcnt(0)
	v_bfe_u32 v120, v226, 16, 1
	v_bfe_u32 v121, v227, 16, 1
	v_bfe_u32 v122, v228, 16, 1
	v_bfe_u32 v123, v229, 16, 1
	v_bfe_u32 v124, v230, 16, 1
	v_bfe_u32 v125, v231, 16, 1
	v_bfe_u32 v126, v232, 16, 1
	v_bfe_u32 v127, v233, 16, 1
	v_add3_u32 v226, v226, v120, s63
	v_add3_u32 v227, v227, v121, s63
	v_add3_u32 v228, v228, v122, s63
	v_add3_u32 v229, v229, v123, s63
	v_add3_u32 v230, v230, v124, s63
	v_add3_u32 v231, v231, v125, s63
	v_add3_u32 v232, v232, v126, s63
	v_add3_u32 v233, v233, v127, s63
	v_perm_b32 v242, v227, v226, s64
	v_perm_b32 v243, v229, v228, s64
	v_perm_b32 v244, v231, v230, s64
	v_perm_b32 v245, v233, v232, s64
	s_nop 0
	global_store_dwordx4 v93, v[242:245], s[6:7]
	ds_read_b32 v226, v118
	ds_read_b32 v227, v118 offset:512
	ds_read_b32 v228, v118 offset:1024
	ds_read_b32 v229, v118 offset:1536
	ds_read_b32 v230, v118 offset:2048
	ds_read_b32 v231, v118 offset:2560
	ds_read_b32 v232, v118 offset:3072
	ds_read_b32 v233, v118 offset:3584
	s_waitcnt lgkmcnt(0)
	v_bfe_u32 v120, v226, 16, 1
	v_bfe_u32 v121, v227, 16, 1
	v_bfe_u32 v122, v228, 16, 1
	v_bfe_u32 v123, v229, 16, 1
	v_bfe_u32 v124, v230, 16, 1
	v_bfe_u32 v125, v231, 16, 1
	v_bfe_u32 v126, v232, 16, 1
	v_bfe_u32 v127, v233, 16, 1
	v_add3_u32 v226, v226, v120, s63
	v_add3_u32 v227, v227, v121, s63
	v_add3_u32 v228, v228, v122, s63
	v_add3_u32 v229, v229, v123, s63
	v_add3_u32 v230, v230, v124, s63
	v_add3_u32 v231, v231, v125, s63
	v_add3_u32 v232, v232, v126, s63
	v_add3_u32 v233, v233, v127, s63
	v_perm_b32 v242, v227, v226, s64
	v_perm_b32 v243, v229, v228, s64
	v_perm_b32 v244, v231, v230, s64
	v_perm_b32 v245, v233, v232, s64
	s_nop 0
	global_store_dwordx4 v94, v[242:245], s[6:7]
	s_waitcnt vmcnt(16)
	v_mul_f32_e32 v176, v42, v176
	v_mul_f32_e32 v177, v42, v177
	v_mul_f32_e32 v178, v42, v178
	v_mul_f32_e32 v179, v42, v179
	ds_write_b128 v210, v[176:179]
	v_mul_f32_e32 v180, v43, v180
	v_mul_f32_e32 v181, v43, v181
	v_mul_f32_e32 v182, v43, v182
	v_mul_f32_e32 v183, v43, v183
	ds_write_b128 v210, v[180:183] offset:1024
	v_mul_f32_e32 v184, v44, v184
	v_mul_f32_e32 v185, v44, v185
	v_mul_f32_e32 v186, v44, v186
	v_mul_f32_e32 v187, v44, v187
	ds_write_b128 v210, v[184:187] offset:2048
	v_mul_f32_e32 v188, v45, v188
	v_mul_f32_e32 v189, v45, v189
	v_mul_f32_e32 v190, v45, v190
	v_mul_f32_e32 v191, v45, v191
	ds_write_b128 v210, v[188:191] offset:3072
	v_mul_f32_e32 v192, v46, v192
	v_mul_f32_e32 v193, v46, v193
	v_mul_f32_e32 v194, v46, v194
	v_mul_f32_e32 v195, v46, v195
	ds_write_b128 v210, v[192:195] offset:4096
	v_mul_f32_e32 v196, v47, v196
	v_mul_f32_e32 v197, v47, v197
	v_mul_f32_e32 v198, v47, v198
	v_mul_f32_e32 v199, v47, v199
	ds_write_b128 v210, v[196:199] offset:5120
	v_mul_f32_e32 v200, v48, v200
	v_mul_f32_e32 v201, v48, v201
	v_mul_f32_e32 v202, v48, v202
	v_mul_f32_e32 v203, v48, v203
	ds_write_b128 v210, v[200:203] offset:6144
	v_mul_f32_e32 v204, v49, v204
	v_mul_f32_e32 v205, v49, v205
	v_mul_f32_e32 v206, v49, v206
	v_mul_f32_e32 v207, v49, v207
	ds_write_b128 v210, v[204:207] offset:7168
	s_waitcnt lgkmcnt(0)
	s_barrier
; #define GAS __attribute__((address_space(1)))
; #define LAS __attribute__((address_space(3)))
; #define LDS_WAIT() asm volatile("s_waitcnt lgkmcnt(0)" ::: "memory")
; __device__ __forceinline__ unsigned pk2(float lo, float hi) { return f2bf(lo) | (f2bf(hi) << 16); }
; __device__ __forceinline__ int nat_dim(int p) { return (p >> 1) + 64 * (p & 1); }
; __device__ __forceinline__ int src_col_in(int c) {
;     if (c < 5120) { const int blk = c >> 7, p = c & 127; const bool rope = blk < 16 || ((((blk - 16) >> 2) & 1) == 0); const int d = rope ? (p >> 1) + 64 * (p & 1) : p; return blk * 128 + d; }
;     if (c < OFF_Z) return c + 2096;
;     if (c < OFF_G) return c - 4048;
;     if (c < OFF_DT) return 5120 + (c - OFF_G);
;     if (c < NSRC) return c;
;     return -1;
; }
; template <int MAP, bool KS, bool KPERM = false>
; __device__ __forceinline__ void p0_transpose_item(const float* W, int K, int Nsrc, int nblk, bf16* WT, const float* ksA, const float* ksB, int ksplit, LAS float* scr, int item, int lane) {
;     const int kb = item / nblk, nb = item % nblk, k0 = 64 * kb, n0 = 32 * nb;
;     const int nr = n0 + (lane & 31); const int sc = MAP == 1 ? src_col_in(nr) : (MAP == 2 ? nat_dim(nr) : nr);
;     float v[32];
; #pragma unroll
;     for (int i = 0; i < 32; ++i) { const int k = k0 + 2 * i + (lane >> 5); const int ksrc = KPERM ? ((k & ~127) + nat_dim(k & 127)) : k;
;         v[i] = sc >= 0 ? W[(size_t)ksrc * Nsrc + sc] : 0.f; }
; #pragma unroll
;     for (int i = 0; i < 32; ++i) { const int kk = 2 * i + (lane >> 5); const int k = k0 + kk;
;         if (KS) v[i] *= (k < ksplit ? ksA[k] : ksB[k - ksplit]);
;         scr[kk * 33 + (lane & 31)] = v[i]; }
;     LDS_WAIT(); asm volatile("" ::: "memory");
;     const int c = lane & 7;
; #pragma unroll
;     for (int j = 0; j < 4; ++j) { const int n = (lane >> 3) + 8 * j; const LAS float* s = scr + (8 * c) * 33 + n;
;         v4u o; o.x = pk2(s[0 * 33], s[1 * 33]); o.y = pk2(s[2 * 33], s[3 * 33]); o.z = pk2(s[4 * 33], s[5 * 33]); o.w = pk2(s[6 * 33], s[7 * 33]);
;         *(GAS v4u*)(WT + (size_t)(n0 + n) * K + k0 + 8 * c) = o; }
;     LDS_WAIT(); asm volatile("" ::: "memory");
; }
	s_add_i32 s24, s23, 72
	s_lshl_b32 s20, s24, 7
	s_cmp_lt_u32 s24, 40
	s_cselect_b32 s21, 0, 0x830
	s_cmp_lt_u32 s24, 72
	s_cselect_b32 s21, s21, 0xfffff030
	s_add_i32 s20, s20, s21
	s_lshl_b32 s20, s20, 2
	s_add_u32 s8, s46, s20
	s_addc_u32 s9, s47, 0
	global_load_dwordx4 v[176:179], v76, s[8:9]
	s_add_u32 s8, s8, 0x16280
	s_addc_u32 s9, s9, 0
	global_load_dwordx4 v[180:183], v76, s[8:9]
	s_add_u32 s8, s8, 0x16280
	s_addc_u32 s9, s9, 0
	global_load_dwordx4 v[184:187], v76, s[8:9]
	s_add_u32 s8, s8, 0x16280
	s_addc_u32 s9, s9, 0
	global_load_dwordx4 v[188:191], v76, s[8:9]
	s_add_u32 s8, s8, 0x16280
	s_addc_u32 s9, s9, 0
	global_load_dwordx4 v[192:195], v76, s[8:9]
	s_add_u32 s8, s8, 0x16280
	s_addc_u32 s9, s9, 0
	global_load_dwordx4 v[196:199], v76, s[8:9]
	s_add_u32 s8, s8, 0x16280
	s_addc_u32 s9, s9, 0
	global_load_dwordx4 v[200:203], v76, s[8:9]
	s_add_u32 s8, s8, 0x16280
	s_addc_u32 s9, s9, 0
	global_load_dwordx4 v[204:207], v76, s[8:9]
	s_add_i32 s24, s23, 56
	s_mul_i32 s20, s24, 0x100000
	s_add_u32 s6, s48, s20
	s_addc_u32 s7, s49, 0
	s_cmp_lt_u32 s24, 16
	s_cselect_b32 s20, 1, 0
	s_sub_i32 s21, s24, 16
	s_bitcmp0_b32 s21, 2
	s_cselect_b32 s21, 1, 0
	s_cmp_lt_u32 s24, 40
	s_cselect_b32 s21, s21, 0
	s_or_b32 s20, s20, s21
	s_cmp_lg_u32 s20, 0
	s_cselect_b64 s[20:21], -1, 0
	v_cndmask_b32_e64 v91, v83, v87, s[20:21]
	v_cndmask_b32_e64 v92, v84, v88, s[20:21]
	v_cndmask_b32_e64 v93, v85, v89, s[20:21]
	v_cndmask_b32_e64 v94, v86, v90, s[20:21]
	ds_read_b32 v226, v113
	ds_read_b32 v227, v113 offset:512
	ds_read_b32 v228, v113 offset:1024
	ds_read_b32 v229, v113 offset:1536
	ds_read_b32 v230, v113 offset:2048
	ds_read_b32 v231, v113 offset:2560
	ds_read_b32 v232, v113 offset:3072
	ds_read_b32 v233, v113 offset:3584
	s_waitcnt lgkmcnt(0)
	v_bfe_u32 v120, v226, 16, 1
	v_bfe_u32 v121, v227, 16, 1
	v_bfe_u32 v122, v228, 16, 1
	v_bfe_u32 v123, v229, 16, 1
	v_bfe_u32 v124, v230, 16, 1
	v_bfe_u32 v125, v231, 16, 1
	v_bfe_u32 v126, v232, 16, 1
	v_bfe_u32 v127, v233, 16, 1
	v_add3_u32 v226, v226, v120, s63
	v_add3_u32 v227, v227, v121, s63
	v_add3_u32 v228, v228, v122, s63
	v_add3_u32 v229, v229, v123, s63
	v_add3_u32 v230, v230, v124, s63
	v_add3_u32 v231, v231, v125, s63
	v_add3_u32 v232, v232, v126, s63
	v_add3_u32 v233, v233, v127, s63
	v_perm_b32 v242, v227, v226, s64
	v_perm_b32 v243, v229, v228, s64
	v_perm_b32 v244, v231, v230, s64
	v_perm_b32 v245, v233, v232, s64
	s_nop 0
	global_store_dwordx4 v91, v[242:245], s[6:7]
	ds_read_b32 v226, v115
	ds_read_b32 v227, v115 offset:512
	ds_read_b32 v228, v115 offset:1024
	ds_read_b32 v229, v115 offset:1536
	ds_read_b32 v230, v115 offset:2048
	ds_read_b32 v231, v115 offset:2560
	ds_read_b32 v232, v115 offset:3072
	ds_read_b32 v233, v115 offset:3584
	s_waitcnt lgkmcnt(0)
	v_bfe_u32 v120, v226, 16, 1
	v_bfe_u32 v121, v227, 16, 1
	v_bfe_u32 v122, v228, 16, 1
	v_bfe_u32 v123, v229, 16, 1
	v_bfe_u32 v124, v230, 16, 1
	v_bfe_u32 v125, v231, 16, 1
	v_bfe_u32 v126, v232, 16, 1
	v_bfe_u32 v127, v233, 16, 1
	v_add3_u32 v226, v226, v120, s63
	v_add3_u32 v227, v227, v121, s63
	v_add3_u32 v228, v228, v122, s63
	v_add3_u32 v229, v229, v123, s63
	v_add3_u32 v230, v230, v124, s63
	v_add3_u32 v231, v231, v125, s63
	v_add3_u32 v232, v232, v126, s63
	v_add3_u32 v233, v233, v127, s63
	v_perm_b32 v242, v227, v226, s64
	v_perm_b32 v243, v229, v228, s64
	v_perm_b32 v244, v231, v230, s64
	v_perm_b32 v245, v233, v232, s64
	s_nop 0
	global_store_dwordx4 v92, v[242:245], s[6:7]
	ds_read_b32 v226, v117
	ds_read_b32 v227, v117 offset:512
	ds_read_b32 v228, v117 offset:1024
	ds_read_b32 v229, v117 offset:1536
	ds_read_b32 v230, v117 offset:2048
	ds_read_b32 v231, v117 offset:2560
	ds_read_b32 v232, v117 offset:3072
	ds_read_b32 v233, v117 offset:3584
	s_waitcnt lgkmcnt(0)
	v_bfe_u32 v120, v226, 16, 1
	v_bfe_u32 v121, v227, 16, 1
	v_bfe_u32 v122, v228, 16, 1
	v_bfe_u32 v123, v229, 16, 1
	v_bfe_u32 v124, v230, 16, 1
	v_bfe_u32 v125, v231, 16, 1
	v_bfe_u32 v126, v232, 16, 1
	v_bfe_u32 v127, v233, 16, 1
	v_add3_u32 v226, v226, v120, s63
	v_add3_u32 v227, v227, v121, s63
	v_add3_u32 v228, v228, v122, s63
	v_add3_u32 v229, v229, v123, s63
	v_add3_u32 v230, v230, v124, s63
	v_add3_u32 v231, v231, v125, s63
	v_add3_u32 v232, v232, v126, s63
	v_add3_u32 v233, v233, v127, s63
	v_perm_b32 v242, v227, v226, s64
	v_perm_b32 v243, v229, v228, s64
	v_perm_b32 v244, v231, v230, s64
	v_perm_b32 v245, v233, v232, s64
	s_nop 0
	global_store_dwordx4 v93, v[242:245], s[6:7]
	ds_read_b32 v226, v119
	ds_read_b32 v227, v119 offset:512
	ds_read_b32 v228, v119 offset:1024
	ds_read_b32 v229, v119 offset:1536
	ds_read_b32 v230, v119 offset:2048
	ds_read_b32 v231, v119 offset:2560
	ds_read_b32 v232, v119 offset:3072
	ds_read_b32 v233, v119 offset:3584
	s_waitcnt lgkmcnt(0)
	v_bfe_u32 v120, v226, 16, 1
	v_bfe_u32 v121, v227, 16, 1
	v_bfe_u32 v122, v228, 16, 1
	v_bfe_u32 v123, v229, 16, 1
	v_bfe_u32 v124, v230, 16, 1
	v_bfe_u32 v125, v231, 16, 1
	v_bfe_u32 v126, v232, 16, 1
	v_bfe_u32 v127, v233, 16, 1
	v_add3_u32 v226, v226, v120, s63
	v_add3_u32 v227, v227, v121, s63
	v_add3_u32 v228, v228, v122, s63
	v_add3_u32 v229, v229, v123, s63
	v_add3_u32 v230, v230, v124, s63
	v_add3_u32 v231, v231, v125, s63
	v_add3_u32 v232, v232, v126, s63
	v_add3_u32 v233, v233, v127, s63
	v_perm_b32 v242, v227, v226, s64
	v_perm_b32 v243, v229, v228, s64
	v_perm_b32 v244, v231, v230, s64
	v_perm_b32 v245, v233, v232, s64
	s_nop 0
	global_store_dwordx4 v94, v[242:245], s[6:7]
	s_waitcnt vmcnt(16)
	v_mul_f32_e32 v144, v42, v144
	v_mul_f32_e32 v145, v42, v145
	v_mul_f32_e32 v146, v42, v146
	v_mul_f32_e32 v147, v42, v147
	ds_write_b128 v209, v[144:147]
	v_mul_f32_e32 v148, v43, v148
	v_mul_f32_e32 v149, v43, v149
	v_mul_f32_e32 v150, v43, v150
	v_mul_f32_e32 v151, v43, v151
	ds_write_b128 v209, v[148:151] offset:1024
	v_mul_f32_e32 v152, v44, v152
	v_mul_f32_e32 v153, v44, v153
	v_mul_f32_e32 v154, v44, v154
	v_mul_f32_e32 v155, v44, v155
	ds_write_b128 v209, v[152:155] offset:2048
	v_mul_f32_e32 v156, v45, v156
	v_mul_f32_e32 v157, v45, v157
	v_mul_f32_e32 v158, v45, v158
	v_mul_f32_e32 v159, v45, v159
	ds_write_b128 v209, v[156:159] offset:3072
	v_mul_f32_e32 v160, v46, v160
	v_mul_f32_e32 v161, v46, v161
	v_mul_f32_e32 v162, v46, v162
	v_mul_f32_e32 v163, v46, v163
	ds_write_b128 v209, v[160:163] offset:4096
	v_mul_f32_e32 v164, v47, v164
	v_mul_f32_e32 v165, v47, v165
	v_mul_f32_e32 v166, v47, v166
	v_mul_f32_e32 v167, v47, v167
	ds_write_b128 v209, v[164:167] offset:5120
	v_mul_f32_e32 v168, v48, v168
	v_mul_f32_e32 v169, v48, v169
	v_mul_f32_e32 v170, v48, v170
	v_mul_f32_e32 v171, v48, v171
	ds_write_b128 v209, v[168:171] offset:6144
	v_mul_f32_e32 v172, v49, v172
	v_mul_f32_e32 v173, v49, v173
	v_mul_f32_e32 v174, v49, v174
	v_mul_f32_e32 v175, v49, v175
	ds_write_b128 v209, v[172:175] offset:7168
	s_waitcnt lgkmcnt(0)
	s_barrier
; #define GAS __attribute__((address_space(1)))
; #define LAS __attribute__((address_space(3)))
; #define LDS_WAIT() asm volatile("s_waitcnt lgkmcnt(0)" ::: "memory")
; __device__ __forceinline__ unsigned pk2(float lo, float hi) { return f2bf(lo) | (f2bf(hi) << 16); }
; __device__ __forceinline__ int nat_dim(int p) { return (p >> 1) + 64 * (p & 1); }
; __device__ __forceinline__ int src_col_in(int c) {
;     if (c < 5120) { const int blk = c >> 7, p = c & 127; const bool rope = blk < 16 || ((((blk - 16) >> 2) & 1) == 0); const int d = rope ? (p >> 1) + 64 * (p & 1) : p; return blk * 128 + d; }
;     if (c < OFF_Z) return c + 2096;
;     if (c < OFF_G) return c - 4048;
;     if (c < OFF_DT) return 5120 + (c - OFF_G);
;     if (c < NSRC) return c;
;     return -1;
; }
; template <int MAP, bool KS, bool KPERM = false>
; __device__ __forceinline__ void p0_transpose_item(const float* W, int K, int Nsrc, int nblk, bf16* WT, const float* ksA, const float* ksB, int ksplit, LAS float* scr, int item, int lane) {
;     const int kb = item / nblk, nb = item % nblk, k0 = 64 * kb, n0 = 32 * nb;
;     const int nr = n0 + (lane & 31); const int sc = MAP == 1 ? src_col_in(nr) : (MAP == 2 ? nat_dim(nr) : nr);
;     float v[32];
; #pragma unroll
;     for (int i = 0; i < 32; ++i) { const int k = k0 + 2 * i + (lane >> 5); const int ksrc = KPERM ? ((k & ~127) + nat_dim(k & 127)) : k;
;         v[i] = sc >= 0 ? W[(size_t)ksrc * Nsrc + sc] : 0.f; }
; #pragma unroll
;     for (int i = 0; i < 32; ++i) { const int kk = 2 * i + (lane >> 5); const int k = k0 + kk;
;         if (KS) v[i] *= (k < ksplit ? ksA[k] : ksB[k - ksplit]);
;         scr[kk * 33 + (lane & 31)] = v[i]; }
;     LDS_WAIT(); asm volatile("" ::: "memory");
;     const int c = lane & 7;
; #pragma unroll
;     for (int j = 0; j < 4; ++j) { const int n = (lane >> 3) + 8 * j; const LAS float* s = scr + (8 * c) * 33 + n;
;         v4u o; o.x = pk2(s[0 * 33], s[1 * 33]); o.y = pk2(s[2 * 33], s[3 * 33]); o.z = pk2(s[4 * 33], s[5 * 33]); o.w = pk2(s[6 * 33], s[7 * 33]);
;         *(GAS v4u*)(WT + (size_t)(n0 + n) * K + k0 + 8 * c) = o; }
;     LDS_WAIT(); asm volatile("" ::: "memory");
; }
	s_add_i32 s24, s23, 80
	s_lshl_b32 s20, s24, 7
	s_cmp_lt_u32 s24, 40
	s_cselect_b32 s21, 0, 0x830
	s_cmp_lt_u32 s24, 72
	s_cselect_b32 s21, s21, 0xfffff030
	s_add_i32 s20, s20, s21
	s_lshl_b32 s20, s20, 2
	s_add_u32 s8, s46, s20
	s_addc_u32 s9, s47, 0
	global_load_dwordx4 v[144:147], v76, s[8:9]
	s_add_u32 s8, s8, 0x16280
	s_addc_u32 s9, s9, 0
	global_load_dwordx4 v[148:151], v76, s[8:9]
	s_add_u32 s8, s8, 0x16280
	s_addc_u32 s9, s9, 0
	global_load_dwordx4 v[152:155], v76, s[8:9]
	s_add_u32 s8, s8, 0x16280
	s_addc_u32 s9, s9, 0
	global_load_dwordx4 v[156:159], v76, s[8:9]
	s_add_u32 s8, s8, 0x16280
	s_addc_u32 s9, s9, 0
	global_load_dwordx4 v[160:163], v76, s[8:9]
	s_add_u32 s8, s8, 0x16280
	s_addc_u32 s9, s9, 0
	global_load_dwordx4 v[164:167], v76, s[8:9]
	s_add_u32 s8, s8, 0x16280
	s_addc_u32 s9, s9, 0
	global_load_dwordx4 v[168:171], v76, s[8:9]
	s_add_u32 s8, s8, 0x16280
	s_addc_u32 s9, s9, 0
	global_load_dwordx4 v[172:175], v76, s[8:9]
	s_add_i32 s24, s23, 64
	s_mul_i32 s20, s24, 0x100000
	s_add_u32 s6, s48, s20
	s_addc_u32 s7, s49, 0
	s_cmp_lt_u32 s24, 16
	s_cselect_b32 s20, 1, 0
	s_sub_i32 s21, s24, 16
	s_bitcmp0_b32 s21, 2
	s_cselect_b32 s21, 1, 0
	s_cmp_lt_u32 s24, 40
	s_cselect_b32 s21, s21, 0
	s_or_b32 s20, s20, s21
	s_cmp_lg_u32 s20, 0
	s_cselect_b64 s[20:21], -1, 0
	v_cndmask_b32_e64 v91, v83, v87, s[20:21]
	v_cndmask_b32_e64 v92, v84, v88, s[20:21]
	v_cndmask_b32_e64 v93, v85, v89, s[20:21]
	v_cndmask_b32_e64 v94, v86, v90, s[20:21]
	ds_read_b32 v226, v112
	ds_read_b32 v227, v112 offset:512
	ds_read_b32 v228, v112 offset:1024
	ds_read_b32 v229, v112 offset:1536
	ds_read_b32 v230, v112 offset:2048
	ds_read_b32 v231, v112 offset:2560
	ds_read_b32 v232, v112 offset:3072
	ds_read_b32 v233, v112 offset:3584
	s_waitcnt lgkmcnt(0)
	v_bfe_u32 v120, v226, 16, 1
	v_bfe_u32 v121, v227, 16, 1
	v_bfe_u32 v122, v228, 16, 1
	v_bfe_u32 v123, v229, 16, 1
	v_bfe_u32 v124, v230, 16, 1
	v_bfe_u32 v125, v231, 16, 1
	v_bfe_u32 v126, v232, 16, 1
	v_bfe_u32 v127, v233, 16, 1
	v_add3_u32 v226, v226, v120, s63
	v_add3_u32 v227, v227, v121, s63
	v_add3_u32 v228, v228, v122, s63
	v_add3_u32 v229, v229, v123, s63
	v_add3_u32 v230, v230, v124, s63
	v_add3_u32 v231, v231, v125, s63
	v_add3_u32 v232, v232, v126, s63
	v_add3_u32 v233, v233, v127, s63
	v_perm_b32 v242, v227, v226, s64
	v_perm_b32 v243, v229, v228, s64
	v_perm_b32 v244, v231, v230, s64
	v_perm_b32 v245, v233, v232, s64
	s_nop 0
	global_store_dwordx4 v91, v[242:245], s[6:7]
	ds_read_b32 v226, v114
	ds_read_b32 v227, v114 offset:512
	ds_read_b32 v228, v114 offset:1024
	ds_read_b32 v229, v114 offset:1536
	ds_read_b32 v230, v114 offset:2048
	ds_read_b32 v231, v114 offset:2560
	ds_read_b32 v232, v114 offset:3072
	ds_read_b32 v233, v114 offset:3584
	s_waitcnt lgkmcnt(0)
	v_bfe_u32 v120, v226, 16, 1
	v_bfe_u32 v121, v227, 16, 1
	v_bfe_u32 v122, v228, 16, 1
	v_bfe_u32 v123, v229, 16, 1
	v_bfe_u32 v124, v230, 16, 1
	v_bfe_u32 v125, v231, 16, 1
	v_bfe_u32 v126, v232, 16, 1
	v_bfe_u32 v127, v233, 16, 1
	v_add3_u32 v226, v226, v120, s63
	v_add3_u32 v227, v227, v121, s63
	v_add3_u32 v228, v228, v122, s63
	v_add3_u32 v229, v229, v123, s63
	v_add3_u32 v230, v230, v124, s63
	v_add3_u32 v231, v231, v125, s63
	v_add3_u32 v232, v232, v126, s63
	v_add3_u32 v233, v233, v127, s63
	v_perm_b32 v242, v227, v226, s64
	v_perm_b32 v243, v229, v228, s64
	v_perm_b32 v244, v231, v230, s64
	v_perm_b32 v245, v233, v232, s64
	s_nop 0
	global_store_dwordx4 v92, v[242:245], s[6:7]
	ds_read_b32 v226, v116
	ds_read_b32 v227, v116 offset:512
	ds_read_b32 v228, v116 offset:1024
	ds_read_b32 v229, v116 offset:1536
	ds_read_b32 v230, v116 offset:2048
	ds_read_b32 v231, v116 offset:2560
	ds_read_b32 v232, v116 offset:3072
	ds_read_b32 v233, v116 offset:3584
	s_waitcnt lgkmcnt(0)
	v_bfe_u32 v120, v226, 16, 1
	v_bfe_u32 v121, v227, 16, 1
	v_bfe_u32 v122, v228, 16, 1
	v_bfe_u32 v123, v229, 16, 1
	v_bfe_u32 v124, v230, 16, 1
	v_bfe_u32 v125, v231, 16, 1
	v_bfe_u32 v126, v232, 16, 1
	v_bfe_u32 v127, v233, 16, 1
	v_add3_u32 v226, v226, v120, s63
	v_add3_u32 v227, v227, v121, s63
	v_add3_u32 v228, v228, v122, s63
	v_add3_u32 v229, v229, v123, s63
	v_add3_u32 v230, v230, v124, s63
	v_add3_u32 v231, v231, v125, s63
	v_add3_u32 v232, v232, v126, s63
	v_add3_u32 v233, v233, v127, s63
	v_perm_b32 v242, v227, v226, s64
	v_perm_b32 v243, v229, v228, s64
	v_perm_b32 v244, v231, v230, s64
	v_perm_b32 v245, v233, v232, s64
	s_nop 0
	global_store_dwordx4 v93, v[242:245], s[6:7]
	ds_read_b32 v226, v118
	ds_read_b32 v227, v118 offset:512
	ds_read_b32 v228, v118 offset:1024
	ds_read_b32 v229, v118 offset:1536
	ds_read_b32 v230, v118 offset:2048
	ds_read_b32 v231, v118 offset:2560
	ds_read_b32 v232, v118 offset:3072
	ds_read_b32 v233, v118 offset:3584
	s_waitcnt lgkmcnt(0)
	v_bfe_u32 v120, v226, 16, 1
	v_bfe_u32 v121, v227, 16, 1
	v_bfe_u32 v122, v228, 16, 1
	v_bfe_u32 v123, v229, 16, 1
	v_bfe_u32 v124, v230, 16, 1
	v_bfe_u32 v125, v231, 16, 1
	v_bfe_u32 v126, v232, 16, 1
	v_bfe_u32 v127, v233, 16, 1
	v_add3_u32 v226, v226, v120, s63
	v_add3_u32 v227, v227, v121, s63
	v_add3_u32 v228, v228, v122, s63
	v_add3_u32 v229, v229, v123, s63
	v_add3_u32 v230, v230, v124, s63
	v_add3_u32 v231, v231, v125, s63
	v_add3_u32 v232, v232, v126, s63
	v_add3_u32 v233, v233, v127, s63
	v_perm_b32 v242, v227, v226, s64
	v_perm_b32 v243, v229, v228, s64
	v_perm_b32 v244, v231, v230, s64
	v_perm_b32 v245, v233, v232, s64
	s_nop 0
	global_store_dwordx4 v94, v[242:245], s[6:7]
	s_waitcnt vmcnt(16)
	v_mul_f32_e32 v176, v42, v176
	v_mul_f32_e32 v177, v42, v177
	v_mul_f32_e32 v178, v42, v178
	v_mul_f32_e32 v179, v42, v179
	ds_write_b128 v210, v[176:179]
	v_mul_f32_e32 v180, v43, v180
	v_mul_f32_e32 v181, v43, v181
	v_mul_f32_e32 v182, v43, v182
	v_mul_f32_e32 v183, v43, v183
	ds_write_b128 v210, v[180:183] offset:1024
	v_mul_f32_e32 v184, v44, v184
	v_mul_f32_e32 v185, v44, v185
	v_mul_f32_e32 v186, v44, v186
	v_mul_f32_e32 v187, v44, v187
	ds_write_b128 v210, v[184:187] offset:2048
	v_mul_f32_e32 v188, v45, v188
	v_mul_f32_e32 v189, v45, v189
	v_mul_f32_e32 v190, v45, v190
	v_mul_f32_e32 v191, v45, v191
	ds_write_b128 v210, v[188:191] offset:3072
	v_mul_f32_e32 v192, v46, v192
	v_mul_f32_e32 v193, v46, v193
	v_mul_f32_e32 v194, v46, v194
	v_mul_f32_e32 v195, v46, v195
	ds_write_b128 v210, v[192:195] offset:4096
	v_mul_f32_e32 v196, v47, v196
	v_mul_f32_e32 v197, v47, v197
	v_mul_f32_e32 v198, v47, v198
	v_mul_f32_e32 v199, v47, v199
	ds_write_b128 v210, v[196:199] offset:5120
	v_mul_f32_e32 v200, v48, v200
	v_mul_f32_e32 v201, v48, v201
	v_mul_f32_e32 v202, v48, v202
	v_mul_f32_e32 v203, v48, v203
	ds_write_b128 v210, v[200:203] offset:6144
	v_mul_f32_e32 v204, v49, v204
	v_mul_f32_e32 v205, v49, v205
	v_mul_f32_e32 v206, v49, v206
	v_mul_f32_e32 v207, v49, v207
	ds_write_b128 v210, v[204:207] offset:7168
	s_waitcnt lgkmcnt(0)
	s_barrier
; #define GAS __attribute__((address_space(1)))
; #define LAS __attribute__((address_space(3)))
; #define LDS_WAIT() asm volatile("s_waitcnt lgkmcnt(0)" ::: "memory")
; __device__ __forceinline__ unsigned pk2(float lo, float hi) { return f2bf(lo) | (f2bf(hi) << 16); }
; __device__ __forceinline__ int nat_dim(int p) { return (p >> 1) + 64 * (p & 1); }
; __device__ __forceinline__ int src_col_in(int c) {
;     if (c < 5120) { const int blk = c >> 7, p = c & 127; const bool rope = blk < 16 || ((((blk - 16) >> 2) & 1) == 0); const int d = rope ? (p >> 1) + 64 * (p & 1) : p; return blk * 128 + d; }
;     if (c < OFF_Z) return c + 2096;
;     if (c < OFF_G) return c - 4048;
;     if (c < OFF_DT) return 5120 + (c - OFF_G);
;     if (c < NSRC) return c;
;     return -1;
; }
; template <int MAP, bool KS, bool KPERM = false>
; __device__ __forceinline__ void p0_transpose_item(const float* W, int K, int Nsrc, int nblk, bf16* WT, const float* ksA, const float* ksB, int ksplit, LAS float* scr, int item, int lane) {
;     const int kb = item / nblk, nb = item % nblk, k0 = 64 * kb, n0 = 32 * nb;
;     const int nr = n0 + (lane & 31); const int sc = MAP == 1 ? src_col_in(nr) : (MAP == 2 ? nat_dim(nr) : nr);
;     float v[32];
; #pragma unroll
;     for (int i = 0; i < 32; ++i) { const int k = k0 + 2 * i + (lane >> 5); const int ksrc = KPERM ? ((k & ~127) + nat_dim(k & 127)) : k;
;         v[i] = sc >= 0 ? W[(size_t)ksrc * Nsrc + sc] : 0.f; }
; #pragma unroll
;     for (int i = 0; i < 32; ++i) { const int kk = 2 * i + (lane >> 5); const int k = k0 + kk;
;         if (KS) v[i] *= (k < ksplit ? ksA[k] : ksB[k - ksplit]);
;         scr[kk * 33 + (lane & 31)] = v[i]; }
;     LDS_WAIT(); asm volatile("" ::: "memory");
;     const int c = lane & 7;
; #pragma unroll
;     for (int j = 0; j < 4; ++j) { const int n = (lane >> 3) + 8 * j; const LAS float* s = scr + (8 * c) * 33 + n;
;         v4u o; o.x = pk2(s[0 * 33], s[1 * 33]); o.y = pk2(s[2 * 33], s[3 * 33]); o.z = pk2(s[4 * 33], s[5 * 33]); o.w = pk2(s[6 * 33], s[7 * 33]);
;         *(GAS v4u*)(WT + (size_t)(n0 + n) * K + k0 + 8 * c) = o; }
;     LDS_WAIT(); asm volatile("" ::: "memory");
; }
	s_add_i32 s24, s23, 0
	s_lshl_b32 s20, s24, 7
	s_cmp_lt_u32 s24, 40
	s_cselect_b32 s21, 0, 0x830
	s_cmp_lt_u32 s24, 72
	s_cselect_b32 s21, s21, 0xfffff030
	s_add_i32 s20, s20, s21
	s_lshl_b32 s20, s20, 2
	s_add_u32 s8, s50, s20
	s_addc_u32 s9, s51, 0
	global_load_dwordx4 v[176:179], v76, s[8:9]
	s_add_u32 s8, s8, 0x16280
	s_addc_u32 s9, s9, 0
	global_load_dwordx4 v[180:183], v76, s[8:9]
	s_add_u32 s8, s8, 0x16280
	s_addc_u32 s9, s9, 0
	global_load_dwordx4 v[184:187], v76, s[8:9]
	s_add_u32 s8, s8, 0x16280
	s_addc_u32 s9, s9, 0
	global_load_dwordx4 v[188:191], v76, s[8:9]
	s_add_u32 s8, s8, 0x16280
	s_addc_u32 s9, s9, 0
	global_load_dwordx4 v[192:195], v76, s[8:9]
	s_add_u32 s8, s8, 0x16280
	s_addc_u32 s9, s9, 0
	global_load_dwordx4 v[196:199], v76, s[8:9]
	s_add_u32 s8, s8, 0x16280
	s_addc_u32 s9, s9, 0
	global_load_dwordx4 v[200:203], v76, s[8:9]
	s_add_u32 s8, s8, 0x16280
	s_addc_u32 s9, s9, 0
	global_load_dwordx4 v[204:207], v76, s[8:9]
	s_add_i32 s24, s23, 72
	s_mul_i32 s20, s24, 0x100000
	s_add_u32 s6, s48, s20
	s_addc_u32 s7, s49, 0
	s_cmp_lt_u32 s24, 16
	s_cselect_b32 s20, 1, 0
	s_sub_i32 s21, s24, 16
	s_bitcmp0_b32 s21, 2
	s_cselect_b32 s21, 1, 0
	s_cmp_lt_u32 s24, 40
	s_cselect_b32 s21, s21, 0
	s_or_b32 s20, s20, s21
	s_cmp_lg_u32 s20, 0
	s_cselect_b64 s[20:21], -1, 0
	v_cndmask_b32_e64 v91, v83, v87, s[20:21]
	v_cndmask_b32_e64 v92, v84, v88, s[20:21]
	v_cndmask_b32_e64 v93, v85, v89, s[20:21]
	v_cndmask_b32_e64 v94, v86, v90, s[20:21]
	ds_read_b32 v226, v113
	ds_read_b32 v227, v113 offset:512
	ds_read_b32 v228, v113 offset:1024
	ds_read_b32 v229, v113 offset:1536
	ds_read_b32 v230, v113 offset:2048
	ds_read_b32 v231, v113 offset:2560
	ds_read_b32 v232, v113 offset:3072
	ds_read_b32 v233, v113 offset:3584
	s_waitcnt lgkmcnt(0)
	v_bfe_u32 v120, v226, 16, 1
	v_bfe_u32 v121, v227, 16, 1
	v_bfe_u32 v122, v228, 16, 1
	v_bfe_u32 v123, v229, 16, 1
	v_bfe_u32 v124, v230, 16, 1
	v_bfe_u32 v125, v231, 16, 1
	v_bfe_u32 v126, v232, 16, 1
	v_bfe_u32 v127, v233, 16, 1
	v_add3_u32 v226, v226, v120, s63
	v_add3_u32 v227, v227, v121, s63
	v_add3_u32 v228, v228, v122, s63
	v_add3_u32 v229, v229, v123, s63
	v_add3_u32 v230, v230, v124, s63
	v_add3_u32 v231, v231, v125, s63
	v_add3_u32 v232, v232, v126, s63
	v_add3_u32 v233, v233, v127, s63
	v_perm_b32 v242, v227, v226, s64
	v_perm_b32 v243, v229, v228, s64
	v_perm_b32 v244, v231, v230, s64
	v_perm_b32 v245, v233, v232, s64
	s_nop 0
	global_store_dwordx4 v91, v[242:245], s[6:7]
	ds_read_b32 v226, v115
	ds_read_b32 v227, v115 offset:512
	ds_read_b32 v228, v115 offset:1024
	ds_read_b32 v229, v115 offset:1536
	ds_read_b32 v230, v115 offset:2048
	ds_read_b32 v231, v115 offset:2560
	ds_read_b32 v232, v115 offset:3072
	ds_read_b32 v233, v115 offset:3584
	s_waitcnt lgkmcnt(0)
	v_bfe_u32 v120, v226, 16, 1
	v_bfe_u32 v121, v227, 16, 1
	v_bfe_u32 v122, v228, 16, 1
	v_bfe_u32 v123, v229, 16, 1
	v_bfe_u32 v124, v230, 16, 1
	v_bfe_u32 v125, v231, 16, 1
	v_bfe_u32 v126, v232, 16, 1
	v_bfe_u32 v127, v233, 16, 1
	v_add3_u32 v226, v226, v120, s63
	v_add3_u32 v227, v227, v121, s63
	v_add3_u32 v228, v228, v122, s63
	v_add3_u32 v229, v229, v123, s63
	v_add3_u32 v230, v230, v124, s63
	v_add3_u32 v231, v231, v125, s63
	v_add3_u32 v232, v232, v126, s63
	v_add3_u32 v233, v233, v127, s63
	v_perm_b32 v242, v227, v226, s64
	v_perm_b32 v243, v229, v228, s64
	v_perm_b32 v244, v231, v230, s64
	v_perm_b32 v245, v233, v232, s64
	s_nop 0
	global_store_dwordx4 v92, v[242:245], s[6:7]
	ds_read_b32 v226, v117
	ds_read_b32 v227, v117 offset:512
	ds_read_b32 v228, v117 offset:1024
	ds_read_b32 v229, v117 offset:1536
	ds_read_b32 v230, v117 offset:2048
	ds_read_b32 v231, v117 offset:2560
	ds_read_b32 v232, v117 offset:3072
	ds_read_b32 v233, v117 offset:3584
	s_waitcnt lgkmcnt(0)
	v_bfe_u32 v120, v226, 16, 1
	v_bfe_u32 v121, v227, 16, 1
	v_bfe_u32 v122, v228, 16, 1
	v_bfe_u32 v123, v229, 16, 1
	v_bfe_u32 v124, v230, 16, 1
	v_bfe_u32 v125, v231, 16, 1
	v_bfe_u32 v126, v232, 16, 1
	v_bfe_u32 v127, v233, 16, 1
	v_add3_u32 v226, v226, v120, s63
	v_add3_u32 v227, v227, v121, s63
	v_add3_u32 v228, v228, v122, s63
	v_add3_u32 v229, v229, v123, s63
	v_add3_u32 v230, v230, v124, s63
	v_add3_u32 v231, v231, v125, s63
	v_add3_u32 v232, v232, v126, s63
	v_add3_u32 v233, v233, v127, s63
	v_perm_b32 v242, v227, v226, s64
	v_perm_b32 v243, v229, v228, s64
	v_perm_b32 v244, v231, v230, s64
	v_perm_b32 v245, v233, v232, s64
	s_nop 0
	global_store_dwordx4 v93, v[242:245], s[6:7]
	ds_read_b32 v226, v119
	ds_read_b32 v227, v119 offset:512
	ds_read_b32 v228, v119 offset:1024
	ds_read_b32 v229, v119 offset:1536
	ds_read_b32 v230, v119 offset:2048
	ds_read_b32 v231, v119 offset:2560
	ds_read_b32 v232, v119 offset:3072
	ds_read_b32 v233, v119 offset:3584
	s_waitcnt lgkmcnt(0)
	v_bfe_u32 v120, v226, 16, 1
	v_bfe_u32 v121, v227, 16, 1
	v_bfe_u32 v122, v228, 16, 1
	v_bfe_u32 v123, v229, 16, 1
	v_bfe_u32 v124, v230, 16, 1
	v_bfe_u32 v125, v231, 16, 1
	v_bfe_u32 v126, v232, 16, 1
	v_bfe_u32 v127, v233, 16, 1
	v_add3_u32 v226, v226, v120, s63
	v_add3_u32 v227, v227, v121, s63
	v_add3_u32 v228, v228, v122, s63
	v_add3_u32 v229, v229, v123, s63
	v_add3_u32 v230, v230, v124, s63
	v_add3_u32 v231, v231, v125, s63
	v_add3_u32 v232, v232, v126, s63
	v_add3_u32 v233, v233, v127, s63
	v_perm_b32 v242, v227, v226, s64
	v_perm_b32 v243, v229, v228, s64
	v_perm_b32 v244, v231, v230, s64
	v_perm_b32 v245, v233, v232, s64
	s_nop 0
	global_store_dwordx4 v94, v[242:245], s[6:7]
	s_waitcnt vmcnt(16)
	v_mul_f32_e32 v144, v42, v144
	v_mul_f32_e32 v145, v42, v145
	v_mul_f32_e32 v146, v42, v146
	v_mul_f32_e32 v147, v42, v147
	ds_write_b128 v209, v[144:147]
	v_mul_f32_e32 v148, v43, v148
	v_mul_f32_e32 v149, v43, v149
	v_mul_f32_e32 v150, v43, v150
	v_mul_f32_e32 v151, v43, v151
	ds_write_b128 v209, v[148:151] offset:1024
	v_mul_f32_e32 v152, v44, v152
	v_mul_f32_e32 v153, v44, v153
	v_mul_f32_e32 v154, v44, v154
	v_mul_f32_e32 v155, v44, v155
	ds_write_b128 v209, v[152:155] offset:2048
	v_mul_f32_e32 v156, v45, v156
	v_mul_f32_e32 v157, v45, v157
	v_mul_f32_e32 v158, v45, v158
	v_mul_f32_e32 v159, v45, v159
	ds_write_b128 v209, v[156:159] offset:3072
	v_mul_f32_e32 v160, v46, v160
	v_mul_f32_e32 v161, v46, v161
	v_mul_f32_e32 v162, v46, v162
	v_mul_f32_e32 v163, v46, v163
	ds_write_b128 v209, v[160:163] offset:4096
	v_mul_f32_e32 v164, v47, v164
	v_mul_f32_e32 v165, v47, v165
	v_mul_f32_e32 v166, v47, v166
	v_mul_f32_e32 v167, v47, v167
	ds_write_b128 v209, v[164:167] offset:5120
	v_mul_f32_e32 v168, v48, v168
	v_mul_f32_e32 v169, v48, v169
	v_mul_f32_e32 v170, v48, v170
	v_mul_f32_e32 v171, v48, v171
	ds_write_b128 v209, v[168:171] offset:6144
	v_mul_f32_e32 v172, v49, v172
	v_mul_f32_e32 v173, v49, v173
	v_mul_f32_e32 v174, v49, v174
	v_mul_f32_e32 v175, v49, v175
	ds_write_b128 v209, v[172:175] offset:7168
	s_waitcnt lgkmcnt(0)
	s_barrier
; template <int MAP, bool KS, bool KPERM = false>
; __device__ __forceinline__ void p0_transpose_item(const float* W, int K, int Nsrc, int nblk, bf16* WT, const float* ksA, const float* ksB, int ksplit, LAS float* scr, int item, int lane) {
;     const int kb = item / nblk, nb = item % nblk, k0 = 64 * kb, n0 = 32 * nb;
;     const int nr = n0 + (lane & 31); const int sc = MAP == 1 ? src_col_in(nr) : (MAP == 2 ? nat_dim(nr) : nr);
;     float v[32];
; #pragma unroll
;     for (int i = 0; i < 32; ++i) { const int k = k0 + 2 * i + (lane >> 5); const int ksrc = KPERM ? ((k & ~127) + nat_dim(k & 127)) : k;
;         v[i] = sc >= 0 ? W[(size_t)ksrc * Nsrc + sc] : 0.f; }
; #pragma unroll
;     for (int i = 0; i < 32; ++i) { const int kk = 2 * i + (lane >> 5); const int k = k0 + kk;
;         if (KS) v[i] *= (k < ksplit ? ksA[k] : ksB[k - ksplit]);
;         scr[kk * 33 + (lane & 31)] = v[i]; }
;     LDS_WAIT(); asm volatile("" ::: "memory");
;     const int c = lane & 7;
; #pragma unroll
;     for (int j = 0; j < 4; ++j) { const int n = (lane >> 3) + 8 * j; const LAS float* s = scr + (8 * c) * 33 + n;
;         v4u o; o.x = pk2(s[0 * 33], s[1 * 33]); o.y = pk2(s[2 * 33], s[3 * 33]); o.z = pk2(s[4 * 33], s[5 * 33]); o.w = pk2(s[6 * 33], s[7 * 33]);
;         *(GAS v4u*)(WT + (size_t)(n0 + n) * K + k0 + 8 * c) = o; }
;     LDS_WAIT(); asm volatile("" ::: "memory");
; }
;     const int pr = item >> 1, kb = 2 * (pr / nblk) + (item & 1), nb = pr % nblk, k0 = 64 * kb, n0 = 32 * nb;
;     const int nr = n0 + (lane & 31); const int sc = MAP == 1 ? src_col_in(nr) : nr;
;     float v[32];
; #pragma unroll
;     for (int i = 0; i < 32; ++i) v[i] = sc >= 0 ? W[(size_t)(k0 + 2 * i + (lane >> 5)) * Nsrc + sc] : 0.f;
; #pragma unroll
;     for (int i = 0; i < 32; ++i) { const int k = k0 + 2 * i + (lane >> 5); float x = v[i] * wscale; if (KS) x *= (k < ksplit ? ksA[k] : ksB[k - ksplit]); scr[(2 * i + (lane >> 5)) * 33 + (lane & 31)] = x; }
;     LDS_WAIT(); asm volatile("" ::: "memory");
;     const int c = lane & 7;
; #pragma unroll
;     for (int j = 0; j < 4; ++j) { const int n = (lane >> 3) + 8 * j; const LAS float* s = scr + (8 * c) * 33 + n;
;         const unsigned long long o = (unsigned long long)pg8::pk4_fp8(s[0 * 33], s[1 * 33], s[2 * 33], s[3 * 33]) | ((unsigned long long)pg8::pk4_fp8(s[4 * 33], s[5 * 33], s[6 * 33], s[7 * 33]) << 32);
	s_add_i32 s24, s23, 8
	s_lshl_b32 s20, s24, 7
	s_cmp_lt_u32 s24, 40
	s_cselect_b32 s21, 0, 0x830
	s_cmp_lt_u32 s24, 72
	s_cselect_b32 s21, s21, 0xfffff030
	s_add_i32 s20, s20, s21
	s_lshl_b32 s20, s20, 2
	s_add_u32 s8, s50, s20
	s_addc_u32 s9, s51, 0
	global_load_dwordx4 v[144:147], v76, s[8:9]
	s_add_u32 s8, s8, 0x16280
	s_addc_u32 s9, s9, 0
	global_load_dwordx4 v[148:151], v76, s[8:9]
	s_add_u32 s8, s8, 0x16280
	s_addc_u32 s9, s9, 0
	global_load_dwordx4 v[152:155], v76, s[8:9]
	s_add_u32 s8, s8, 0x16280
	s_addc_u32 s9, s9, 0
	global_load_dwordx4 v[156:159], v76, s[8:9]
	s_add_u32 s8, s8, 0x16280
	s_addc_u32 s9, s9, 0
	global_load_dwordx4 v[160:163], v76, s[8:9]
	s_add_u32 s8, s8, 0x16280
	s_addc_u32 s9, s9, 0
	global_load_dwordx4 v[164:167], v76, s[8:9]
	s_add_u32 s8, s8, 0x16280
	s_addc_u32 s9, s9, 0
	global_load_dwordx4 v[168:171], v76, s[8:9]
	s_add_u32 s8, s8, 0x16280
	s_addc_u32 s9, s9, 0
	global_load_dwordx4 v[172:175], v76, s[8:9]
	s_add_i32 s24, s23, 80
	s_mul_i32 s20, s24, 0x100000
	s_add_u32 s6, s48, s20
	s_addc_u32 s7, s49, 0
	s_cmp_lt_u32 s24, 16
	s_cselect_b32 s20, 1, 0
	s_sub_i32 s21, s24, 16
	s_bitcmp0_b32 s21, 2
	s_cselect_b32 s21, 1, 0
	s_cmp_lt_u32 s24, 40
	s_cselect_b32 s21, s21, 0
	s_or_b32 s20, s20, s21
	s_cmp_lg_u32 s20, 0
	s_cselect_b64 s[20:21], -1, 0
	v_cndmask_b32_e64 v91, v83, v87, s[20:21]
	v_cndmask_b32_e64 v92, v84, v88, s[20:21]
	v_cndmask_b32_e64 v93, v85, v89, s[20:21]
	v_cndmask_b32_e64 v94, v86, v90, s[20:21]
	ds_read_b32 v226, v112
	ds_read_b32 v227, v112 offset:512
	ds_read_b32 v228, v112 offset:1024
	ds_read_b32 v229, v112 offset:1536
	ds_read_b32 v230, v112 offset:2048
	ds_read_b32 v231, v112 offset:2560
	ds_read_b32 v232, v112 offset:3072
	ds_read_b32 v233, v112 offset:3584
	s_waitcnt lgkmcnt(0)
	v_bfe_u32 v120, v226, 16, 1
	v_bfe_u32 v121, v227, 16, 1
	v_bfe_u32 v122, v228, 16, 1
	v_bfe_u32 v123, v229, 16, 1
	v_bfe_u32 v124, v230, 16, 1
	v_bfe_u32 v125, v231, 16, 1
	v_bfe_u32 v126, v232, 16, 1
	v_bfe_u32 v127, v233, 16, 1
	v_add3_u32 v226, v226, v120, s63
	v_add3_u32 v227, v227, v121, s63
	v_add3_u32 v228, v228, v122, s63
	v_add3_u32 v229, v229, v123, s63
	v_add3_u32 v230, v230, v124, s63
	v_add3_u32 v231, v231, v125, s63
	v_add3_u32 v232, v232, v126, s63
	v_add3_u32 v233, v233, v127, s63
	v_perm_b32 v242, v227, v226, s64
	v_perm_b32 v243, v229, v228, s64
	v_perm_b32 v244, v231, v230, s64
	v_perm_b32 v245, v233, v232, s64
	s_nop 0
	global_store_dwordx4 v91, v[242:245], s[6:7]
	ds_read_b32 v226, v114
	ds_read_b32 v227, v114 offset:512
	ds_read_b32 v228, v114 offset:1024
	ds_read_b32 v229, v114 offset:1536
	ds_read_b32 v230, v114 offset:2048
	ds_read_b32 v231, v114 offset:2560
	ds_read_b32 v232, v114 offset:3072
	ds_read_b32 v233, v114 offset:3584
	s_waitcnt lgkmcnt(0)
	v_bfe_u32 v120, v226, 16, 1
	v_bfe_u32 v121, v227, 16, 1
	v_bfe_u32 v122, v228, 16, 1
	v_bfe_u32 v123, v229, 16, 1
	v_bfe_u32 v124, v230, 16, 1
	v_bfe_u32 v125, v231, 16, 1
	v_bfe_u32 v126, v232, 16, 1
	v_bfe_u32 v127, v233, 16, 1
	v_add3_u32 v226, v226, v120, s63
	v_add3_u32 v227, v227, v121, s63
	v_add3_u32 v228, v228, v122, s63
	v_add3_u32 v229, v229, v123, s63
	v_add3_u32 v230, v230, v124, s63
	v_add3_u32 v231, v231, v125, s63
	v_add3_u32 v232, v232, v126, s63
	v_add3_u32 v233, v233, v127, s63
	v_perm_b32 v242, v227, v226, s64
	v_perm_b32 v243, v229, v228, s64
	v_perm_b32 v244, v231, v230, s64
	v_perm_b32 v245, v233, v232, s64
	s_nop 0
	global_store_dwordx4 v92, v[242:245], s[6:7]
	ds_read_b32 v226, v116
	ds_read_b32 v227, v116 offset:512
	ds_read_b32 v228, v116 offset:1024
	ds_read_b32 v229, v116 offset:1536
	ds_read_b32 v230, v116 offset:2048
	ds_read_b32 v231, v116 offset:2560
	ds_read_b32 v232, v116 offset:3072
	ds_read_b32 v233, v116 offset:3584
	s_waitcnt lgkmcnt(0)
	v_bfe_u32 v120, v226, 16, 1
	v_bfe_u32 v121, v227, 16, 1
	v_bfe_u32 v122, v228, 16, 1
	v_bfe_u32 v123, v229, 16, 1
	v_bfe_u32 v124, v230, 16, 1
	v_bfe_u32 v125, v231, 16, 1
	v_bfe_u32 v126, v232, 16, 1
	v_bfe_u32 v127, v233, 16, 1
	v_add3_u32 v226, v226, v120, s63
	v_add3_u32 v227, v227, v121, s63
	v_add3_u32 v228, v228, v122, s63
	v_add3_u32 v229, v229, v123, s63
	v_add3_u32 v230, v230, v124, s63
	v_add3_u32 v231, v231, v125, s63
	v_add3_u32 v232, v232, v126, s63
	v_add3_u32 v233, v233, v127, s63
	v_perm_b32 v242, v227, v226, s64
	v_perm_b32 v243, v229, v228, s64
	v_perm_b32 v244, v231, v230, s64
	v_perm_b32 v245, v233, v232, s64
	s_nop 0
	global_store_dwordx4 v93, v[242:245], s[6:7]
	ds_read_b32 v226, v118
	ds_read_b32 v227, v118 offset:512
	ds_read_b32 v228, v118 offset:1024
	ds_read_b32 v229, v118 offset:1536
	ds_read_b32 v230, v118 offset:2048
	ds_read_b32 v231, v118 offset:2560
	ds_read_b32 v232, v118 offset:3072
	ds_read_b32 v233, v118 offset:3584
	s_waitcnt lgkmcnt(0)
	v_bfe_u32 v120, v226, 16, 1
	v_bfe_u32 v121, v227, 16, 1
	v_bfe_u32 v122, v228, 16, 1
	v_bfe_u32 v123, v229, 16, 1
	v_bfe_u32 v124, v230, 16, 1
	v_bfe_u32 v125, v231, 16, 1
	v_bfe_u32 v126, v232, 16, 1
	v_bfe_u32 v127, v233, 16, 1
	v_add3_u32 v226, v226, v120, s63
	v_add3_u32 v227, v227, v121, s63
	v_add3_u32 v228, v228, v122, s63
	v_add3_u32 v229, v229, v123, s63
	v_add3_u32 v230, v230, v124, s63
	v_add3_u32 v231, v231, v125, s63
	v_add3_u32 v232, v232, v126, s63
	v_add3_u32 v233, v233, v127, s63
	v_perm_b32 v242, v227, v226, s64
	v_perm_b32 v243, v229, v228, s64
	v_perm_b32 v244, v231, v230, s64
	v_perm_b32 v245, v233, v232, s64
	s_nop 0
	global_store_dwordx4 v94, v[242:245], s[6:7]
	s_waitcnt vmcnt(16)
	v_mul_f32_e32 v176, v50, v176
	v_mul_f32_e32 v177, v50, v177
	v_mul_f32_e32 v178, v50, v178
	v_mul_f32_e32 v179, v50, v179
	ds_write_b128 v210, v[176:179]
	v_mul_f32_e32 v180, v51, v180
	v_mul_f32_e32 v181, v51, v181
	v_mul_f32_e32 v182, v51, v182
	v_mul_f32_e32 v183, v51, v183
	ds_write_b128 v210, v[180:183] offset:1024
	v_mul_f32_e32 v184, v52, v184
	v_mul_f32_e32 v185, v52, v185
	v_mul_f32_e32 v186, v52, v186
	v_mul_f32_e32 v187, v52, v187
	ds_write_b128 v210, v[184:187] offset:2048
	v_mul_f32_e32 v188, v53, v188
	v_mul_f32_e32 v189, v53, v189
	v_mul_f32_e32 v190, v53, v190
	v_mul_f32_e32 v191, v53, v191
	ds_write_b128 v210, v[188:191] offset:3072
	v_mul_f32_e32 v192, v54, v192
	v_mul_f32_e32 v193, v54, v193
	v_mul_f32_e32 v194, v54, v194
	v_mul_f32_e32 v195, v54, v195
	ds_write_b128 v210, v[192:195] offset:4096
	v_mul_f32_e32 v196, v55, v196
	v_mul_f32_e32 v197, v55, v197
	v_mul_f32_e32 v198, v55, v198
	v_mul_f32_e32 v199, v55, v199
	ds_write_b128 v210, v[196:199] offset:5120
	v_mul_f32_e32 v200, v56, v200
	v_mul_f32_e32 v201, v56, v201
	v_mul_f32_e32 v202, v56, v202
	v_mul_f32_e32 v203, v56, v203
	ds_write_b128 v210, v[200:203] offset:6144
	v_mul_f32_e32 v204, v57, v204
	v_mul_f32_e32 v205, v57, v205
	v_mul_f32_e32 v206, v57, v206
	v_mul_f32_e32 v207, v57, v207
	ds_write_b128 v210, v[204:207] offset:7168
	s_waitcnt lgkmcnt(0)
	s_barrier
; #define GAS __attribute__((address_space(1)))
; #define LAS __attribute__((address_space(3)))
; #define LDS_WAIT() asm volatile("s_waitcnt lgkmcnt(0)" ::: "memory")
; __device__ __forceinline__ int src_col_in(int c) {
;     if (c < 5120) { const int blk = c >> 7, p = c & 127; const bool rope = blk < 16 || ((((blk - 16) >> 2) & 1) == 0); const int d = rope ? (p >> 1) + 64 * (p & 1) : p; return blk * 128 + d; }
;     if (c < OFF_Z) return c + 2096;
;     if (c < OFF_G) return c - 4048;
;     if (c < OFF_DT) return 5120 + (c - OFF_G);
;     if (c < NSRC) return c;
;     return -1;
; }
;     const int pr = item >> 1, kb = 2 * (pr / nblk) + (item & 1), nb = pr % nblk, k0 = 64 * kb, n0 = 32 * nb;
;     const int nr = n0 + (lane & 31); const int sc = MAP == 1 ? src_col_in(nr) : nr;
;     float v[32];
; #pragma unroll
;     for (int i = 0; i < 32; ++i) v[i] = sc >= 0 ? W[(size_t)(k0 + 2 * i + (lane >> 5)) * Nsrc + sc] : 0.f;
; #pragma unroll
;     for (int i = 0; i < 32; ++i) { const int k = k0 + 2 * i + (lane >> 5); float x = v[i] * wscale; if (KS) x *= (k < ksplit ? ksA[k] : ksB[k - ksplit]); scr[(2 * i + (lane >> 5)) * 33 + (lane & 31)] = x; }
;     LDS_WAIT(); asm volatile("" ::: "memory");
;     const int c = lane & 7;
; #pragma unroll
;     for (int j = 0; j < 4; ++j) { const int n = (lane >> 3) + 8 * j; const LAS float* s = scr + (8 * c) * 33 + n;
;         const unsigned long long o = (unsigned long long)pg8::pk4_fp8(s[0 * 33], s[1 * 33], s[2 * 33], s[3 * 33]) | ((unsigned long long)pg8::pk4_fp8(s[4 * 33], s[5 * 33], s[6 * 33], s[7 * 33]) << 32);
;         *(GAS unsigned long long*)(WT + (size_t)(n0 + n) * K + k0 + 8 * c) = o; }
;     LDS_WAIT(); asm volatile("" ::: "memory");
; }
	s_add_i32 s24, s23, 16
	s_lshl_b32 s20, s24, 7
	s_cmp_lt_u32 s24, 40
	s_cselect_b32 s21, 0, 0x830
	s_cmp_lt_u32 s24, 72
	s_cselect_b32 s21, s21, 0xfffff030
	s_add_i32 s20, s20, s21
	s_lshl_b32 s20, s20, 2
	s_add_u32 s8, s50, s20
	s_addc_u32 s9, s51, 0
	global_load_dwordx4 v[176:179], v76, s[8:9]
	s_add_u32 s8, s8, 0x16280
	s_addc_u32 s9, s9, 0
	global_load_dwordx4 v[180:183], v76, s[8:9]
	s_add_u32 s8, s8, 0x16280
	s_addc_u32 s9, s9, 0
	global_load_dwordx4 v[184:187], v76, s[8:9]
	s_add_u32 s8, s8, 0x16280
	s_addc_u32 s9, s9, 0
	global_load_dwordx4 v[188:191], v76, s[8:9]
	s_add_u32 s8, s8, 0x16280
	s_addc_u32 s9, s9, 0
	global_load_dwordx4 v[192:195], v76, s[8:9]
	s_add_u32 s8, s8, 0x16280
	s_addc_u32 s9, s9, 0
	global_load_dwordx4 v[196:199], v76, s[8:9]
	s_add_u32 s8, s8, 0x16280
	s_addc_u32 s9, s9, 0
	global_load_dwordx4 v[200:203], v76, s[8:9]
	s_add_u32 s8, s8, 0x16280
	s_addc_u32 s9, s9, 0
	global_load_dwordx4 v[204:207], v76, s[8:9]
	s_add_i32 s24, s23, 0
	s_mul_i32 s20, s24, 0x80000
	s_add_u32 s6, s52, s20
	s_addc_u32 s7, s53, 0
	s_cmp_lt_u32 s24, 16
	s_cselect_b32 s20, 1, 0
	s_sub_i32 s21, s24, 16
	s_bitcmp0_b32 s21, 2
	s_cselect_b32 s21, 1, 0
	s_cmp_lt_u32 s24, 40
	s_cselect_b32 s21, s21, 0
	s_or_b32 s20, s20, s21
	s_cmp_lg_u32 s20, 0
	s_cselect_b64 s[20:21], -1, 0
	v_cndmask_b32_e64 v91, v77, v81, s[20:21]
	v_cndmask_b32_e64 v92, v78, v82, s[20:21]
	ds_read_b32 v226, v212
	ds_read_b32 v227, v212 offset:512
	ds_read_b32 v228, v212 offset:1024
	ds_read_b32 v229, v212 offset:1536
	ds_read_b32 v230, v212 offset:2048
	ds_read_b32 v231, v212 offset:2560
	ds_read_b32 v232, v212 offset:3072
	ds_read_b32 v233, v212 offset:3584
	ds_read_b32 v234, v212 offset:4096
	ds_read_b32 v235, v212 offset:4608
	ds_read_b32 v236, v212 offset:5120
	ds_read_b32 v237, v212 offset:5632
	ds_read_b32 v238, v212 offset:6144
	ds_read_b32 v239, v212 offset:6656
	ds_read_b32 v240, v212 offset:7168
	ds_read_b32 v241, v212 offset:7680
	s_waitcnt lgkmcnt(0)
	v_max_f32_e32 v226, v226, v226
	v_max_f32_e32 v227, v227, v227
	v_max_f32_e32 v228, v228, v228
	v_max_f32_e32 v229, v229, v229
	v_max_f32_e32 v230, v230, v230
	v_max_f32_e32 v231, v231, v231
	v_max_f32_e32 v232, v232, v232
	v_max_f32_e32 v233, v233, v233
	v_max_f32_e32 v234, v234, v234
	v_max_f32_e32 v235, v235, v235
	v_max_f32_e32 v236, v236, v236
	v_max_f32_e32 v237, v237, v237
	v_max_f32_e32 v238, v238, v238
	v_max_f32_e32 v239, v239, v239
	v_max_f32_e32 v240, v240, v240
	v_max_f32_e32 v241, v241, v241
	v_med3_f32 v226, v226, s62, v95
	v_med3_f32 v227, v227, s62, v95
	v_med3_f32 v228, v228, s62, v95
	v_med3_f32 v229, v229, s62, v95
	v_med3_f32 v230, v230, s62, v95
	v_med3_f32 v231, v231, s62, v95
	v_med3_f32 v232, v232, s62, v95
	v_med3_f32 v233, v233, s62, v95
	v_med3_f32 v234, v234, s62, v95
	v_med3_f32 v235, v235, s62, v95
	v_med3_f32 v236, v236, s62, v95
	v_med3_f32 v237, v237, s62, v95
	v_med3_f32 v238, v238, s62, v95
	v_med3_f32 v239, v239, s62, v95
	v_med3_f32 v240, v240, s62, v95
	v_med3_f32 v241, v241, s62, v95
	v_mov_b32_e32 v242, 0
	v_mov_b32_e32 v243, 0
	v_mov_b32_e32 v244, 0
	v_mov_b32_e32 v245, 0
	v_cvt_pk_fp8_f32 v242, v226, v227
	v_cvt_pk_fp8_f32 v243, v230, v231
	v_cvt_pk_fp8_f32 v244, v234, v235
	v_cvt_pk_fp8_f32 v245, v238, v239
	v_cvt_pk_fp8_f32 v242, v228, v229 op_sel:[0,0,1]
	v_cvt_pk_fp8_f32 v243, v232, v233 op_sel:[0,0,1]
	v_cvt_pk_fp8_f32 v244, v236, v237 op_sel:[0,0,1]
	v_cvt_pk_fp8_f32 v245, v240, v241 op_sel:[0,0,1]
	s_nop 0
	global_store_dwordx4 v91, v[242:245], s[6:7]
	ds_read_b32 v226, v214
	ds_read_b32 v227, v214 offset:512
	ds_read_b32 v228, v214 offset:1024
	ds_read_b32 v229, v214 offset:1536
	ds_read_b32 v230, v214 offset:2048
	ds_read_b32 v231, v214 offset:2560
	ds_read_b32 v232, v214 offset:3072
	ds_read_b32 v233, v214 offset:3584
	ds_read_b32 v234, v214 offset:4096
	ds_read_b32 v235, v214 offset:4608
	ds_read_b32 v236, v214 offset:5120
	ds_read_b32 v237, v214 offset:5632
	ds_read_b32 v238, v214 offset:6144
	ds_read_b32 v239, v214 offset:6656
	ds_read_b32 v240, v214 offset:7168
	ds_read_b32 v241, v214 offset:7680
	s_waitcnt lgkmcnt(0)
	v_max_f32_e32 v226, v226, v226
	v_max_f32_e32 v227, v227, v227
	v_max_f32_e32 v228, v228, v228
	v_max_f32_e32 v229, v229, v229
	v_max_f32_e32 v230, v230, v230
	v_max_f32_e32 v231, v231, v231
	v_max_f32_e32 v232, v232, v232
	v_max_f32_e32 v233, v233, v233
	v_max_f32_e32 v234, v234, v234
	v_max_f32_e32 v235, v235, v235
	v_max_f32_e32 v236, v236, v236
	v_max_f32_e32 v237, v237, v237
	v_max_f32_e32 v238, v238, v238
	v_max_f32_e32 v239, v239, v239
	v_max_f32_e32 v240, v240, v240
	v_max_f32_e32 v241, v241, v241
	v_med3_f32 v226, v226, s62, v95
	v_med3_f32 v227, v227, s62, v95
	v_med3_f32 v228, v228, s62, v95
	v_med3_f32 v229, v229, s62, v95
	v_med3_f32 v230, v230, s62, v95
	v_med3_f32 v231, v231, s62, v95
	v_med3_f32 v232, v232, s62, v95
	v_med3_f32 v233, v233, s62, v95
	v_med3_f32 v234, v234, s62, v95
	v_med3_f32 v235, v235, s62, v95
	v_med3_f32 v236, v236, s62, v95
	v_med3_f32 v237, v237, s62, v95
	v_med3_f32 v238, v238, s62, v95
	v_med3_f32 v239, v239, s62, v95
	v_med3_f32 v240, v240, s62, v95
	v_med3_f32 v241, v241, s62, v95
	v_mov_b32_e32 v242, 0
	v_mov_b32_e32 v243, 0
	v_mov_b32_e32 v244, 0
	v_mov_b32_e32 v245, 0
	v_cvt_pk_fp8_f32 v242, v226, v227
	v_cvt_pk_fp8_f32 v243, v230, v231
	v_cvt_pk_fp8_f32 v244, v234, v235
	v_cvt_pk_fp8_f32 v245, v238, v239
	v_cvt_pk_fp8_f32 v242, v228, v229 op_sel:[0,0,1]
	v_cvt_pk_fp8_f32 v243, v232, v233 op_sel:[0,0,1]
	v_cvt_pk_fp8_f32 v244, v236, v237 op_sel:[0,0,1]
	v_cvt_pk_fp8_f32 v245, v240, v241 op_sel:[0,0,1]
	s_nop 0
	global_store_dwordx4 v92, v[242:245], s[6:7]
	s_waitcnt vmcnt(14)
	v_mul_f32_e32 v144, v50, v144
	v_mul_f32_e32 v145, v50, v145
	v_mul_f32_e32 v146, v50, v146
	v_mul_f32_e32 v147, v50, v147
	ds_write_b128 v209, v[144:147]
	v_mul_f32_e32 v148, v51, v148
	v_mul_f32_e32 v149, v51, v149
	v_mul_f32_e32 v150, v51, v150
	v_mul_f32_e32 v151, v51, v151
	ds_write_b128 v209, v[148:151] offset:1024
	v_mul_f32_e32 v152, v52, v152
	v_mul_f32_e32 v153, v52, v153
	v_mul_f32_e32 v154, v52, v154
	v_mul_f32_e32 v155, v52, v155
	ds_write_b128 v209, v[152:155] offset:2048
	v_mul_f32_e32 v156, v53, v156
	v_mul_f32_e32 v157, v53, v157
	v_mul_f32_e32 v158, v53, v158
	v_mul_f32_e32 v159, v53, v159
	ds_write_b128 v209, v[156:159] offset:3072
	v_mul_f32_e32 v160, v54, v160
	v_mul_f32_e32 v161, v54, v161
	v_mul_f32_e32 v162, v54, v162
	v_mul_f32_e32 v163, v54, v163
	ds_write_b128 v209, v[160:163] offset:4096
	v_mul_f32_e32 v164, v55, v164
	v_mul_f32_e32 v165, v55, v165
	v_mul_f32_e32 v166, v55, v166
	v_mul_f32_e32 v167, v55, v167
	ds_write_b128 v209, v[164:167] offset:5120
	v_mul_f32_e32 v168, v56, v168
	v_mul_f32_e32 v169, v56, v169
	v_mul_f32_e32 v170, v56, v170
	v_mul_f32_e32 v171, v56, v171
	ds_write_b128 v209, v[168:171] offset:6144
	v_mul_f32_e32 v172, v57, v172
	v_mul_f32_e32 v173, v57, v173
	v_mul_f32_e32 v174, v57, v174
	v_mul_f32_e32 v175, v57, v175
	ds_write_b128 v209, v[172:175] offset:7168
	s_waitcnt lgkmcnt(0)
	s_barrier
; #define GAS __attribute__((address_space(1)))
; #define LAS __attribute__((address_space(3)))
; #define LDS_WAIT() asm volatile("s_waitcnt lgkmcnt(0)" ::: "memory")
; __device__ __forceinline__ int src_col_in(int c) {
;     if (c < 5120) { const int blk = c >> 7, p = c & 127; const bool rope = blk < 16 || ((((blk - 16) >> 2) & 1) == 0); const int d = rope ? (p >> 1) + 64 * (p & 1) : p; return blk * 128 + d; }
;     if (c < OFF_Z) return c + 2096;
;     if (c < OFF_G) return c - 4048;
;     if (c < OFF_DT) return 5120 + (c - OFF_G);
;     if (c < NSRC) return c;
;     return -1;
; }
;     const int pr = item >> 1, kb = 2 * (pr / nblk) + (item & 1), nb = pr % nblk, k0 = 64 * kb, n0 = 32 * nb;
;     const int nr = n0 + (lane & 31); const int sc = MAP == 1 ? src_col_in(nr) : nr;
;     float v[32];
; #pragma unroll
;     for (int i = 0; i < 32; ++i) v[i] = sc >= 0 ? W[(size_t)(k0 + 2 * i + (lane >> 5)) * Nsrc + sc] : 0.f;
; #pragma unroll
;     for (int i = 0; i < 32; ++i) { const int k = k0 + 2 * i + (lane >> 5); float x = v[i] * wscale; if (KS) x *= (k < ksplit ? ksA[k] : ksB[k - ksplit]); scr[(2 * i + (lane >> 5)) * 33 + (lane & 31)] = x; }
;     LDS_WAIT(); asm volatile("" ::: "memory");
;     const int c = lane & 7;
; #pragma unroll
;     for (int j = 0; j < 4; ++j) { const int n = (lane >> 3) + 8 * j; const LAS float* s = scr + (8 * c) * 33 + n;
;         const unsigned long long o = (unsigned long long)pg8::pk4_fp8(s[0 * 33], s[1 * 33], s[2 * 33], s[3 * 33]) | ((unsigned long long)pg8::pk4_fp8(s[4 * 33], s[5 * 33], s[6 * 33], s[7 * 33]) << 32);
;         *(GAS unsigned long long*)(WT + (size_t)(n0 + n) * K + k0 + 8 * c) = o; }
;     LDS_WAIT(); asm volatile("" ::: "memory");
; }
	s_add_i32 s24, s23, 24
	s_lshl_b32 s20, s24, 7
	s_cmp_lt_u32 s24, 40
	s_cselect_b32 s21, 0, 0x830
	s_cmp_lt_u32 s24, 72
	s_cselect_b32 s21, s21, 0xfffff030
	s_add_i32 s20, s20, s21
	s_lshl_b32 s20, s20, 2
	s_add_u32 s8, s50, s20
	s_addc_u32 s9, s51, 0
	global_load_dwordx4 v[144:147], v76, s[8:9]
	s_add_u32 s8, s8, 0x16280
	s_addc_u32 s9, s9, 0
	global_load_dwordx4 v[148:151], v76, s[8:9]
	s_add_u32 s8, s8, 0x16280
	s_addc_u32 s9, s9, 0
	global_load_dwordx4 v[152:155], v76, s[8:9]
	s_add_u32 s8, s8, 0x16280
	s_addc_u32 s9, s9, 0
	global_load_dwordx4 v[156:159], v76, s[8:9]
	s_add_u32 s8, s8, 0x16280
	s_addc_u32 s9, s9, 0
	global_load_dwordx4 v[160:163], v76, s[8:9]
	s_add_u32 s8, s8, 0x16280
	s_addc_u32 s9, s9, 0
	global_load_dwordx4 v[164:167], v76, s[8:9]
	s_add_u32 s8, s8, 0x16280
	s_addc_u32 s9, s9, 0
	global_load_dwordx4 v[168:171], v76, s[8:9]
	s_add_u32 s8, s8, 0x16280
	s_addc_u32 s9, s9, 0
	global_load_dwordx4 v[172:175], v76, s[8:9]
	s_add_i32 s24, s23, 8
	s_mul_i32 s20, s24, 0x80000
	s_add_u32 s6, s52, s20
	s_addc_u32 s7, s53, 0
	s_cmp_lt_u32 s24, 16
	s_cselect_b32 s20, 1, 0
	s_sub_i32 s21, s24, 16
	s_bitcmp0_b32 s21, 2
	s_cselect_b32 s21, 1, 0
	s_cmp_lt_u32 s24, 40
	s_cselect_b32 s21, s21, 0
	s_or_b32 s20, s20, s21
	s_cmp_lg_u32 s20, 0
	s_cselect_b64 s[20:21], -1, 0
	v_cndmask_b32_e64 v91, v77, v81, s[20:21]
	v_cndmask_b32_e64 v92, v78, v82, s[20:21]
	ds_read_b32 v226, v211
	ds_read_b32 v227, v211 offset:512
	ds_read_b32 v228, v211 offset:1024
	ds_read_b32 v229, v211 offset:1536
	ds_read_b32 v230, v211 offset:2048
	ds_read_b32 v231, v211 offset:2560
	ds_read_b32 v232, v211 offset:3072
	ds_read_b32 v233, v211 offset:3584
	ds_read_b32 v234, v211 offset:4096
	ds_read_b32 v235, v211 offset:4608
	ds_read_b32 v236, v211 offset:5120
	ds_read_b32 v237, v211 offset:5632
	ds_read_b32 v238, v211 offset:6144
	ds_read_b32 v239, v211 offset:6656
	ds_read_b32 v240, v211 offset:7168
	ds_read_b32 v241, v211 offset:7680
	s_waitcnt lgkmcnt(0)
	v_max_f32_e32 v226, v226, v226
	v_max_f32_e32 v227, v227, v227
	v_max_f32_e32 v228, v228, v228
	v_max_f32_e32 v229, v229, v229
	v_max_f32_e32 v230, v230, v230
	v_max_f32_e32 v231, v231, v231
	v_max_f32_e32 v232, v232, v232
	v_max_f32_e32 v233, v233, v233
	v_max_f32_e32 v234, v234, v234
	v_max_f32_e32 v235, v235, v235
	v_max_f32_e32 v236, v236, v236
	v_max_f32_e32 v237, v237, v237
	v_max_f32_e32 v238, v238, v238
	v_max_f32_e32 v239, v239, v239
	v_max_f32_e32 v240, v240, v240
	v_max_f32_e32 v241, v241, v241
	v_med3_f32 v226, v226, s62, v95
	v_med3_f32 v227, v227, s62, v95
	v_med3_f32 v228, v228, s62, v95
	v_med3_f32 v229, v229, s62, v95
	v_med3_f32 v230, v230, s62, v95
	v_med3_f32 v231, v231, s62, v95
	v_med3_f32 v232, v232, s62, v95
	v_med3_f32 v233, v233, s62, v95
	v_med3_f32 v234, v234, s62, v95
	v_med3_f32 v235, v235, s62, v95
	v_med3_f32 v236, v236, s62, v95
	v_med3_f32 v237, v237, s62, v95
	v_med3_f32 v238, v238, s62, v95
	v_med3_f32 v239, v239, s62, v95
	v_med3_f32 v240, v240, s62, v95
	v_med3_f32 v241, v241, s62, v95
	v_mov_b32_e32 v242, 0
	v_mov_b32_e32 v243, 0
	v_mov_b32_e32 v244, 0
	v_mov_b32_e32 v245, 0
	v_cvt_pk_fp8_f32 v242, v226, v227
	v_cvt_pk_fp8_f32 v243, v230, v231
	v_cvt_pk_fp8_f32 v244, v234, v235
	v_cvt_pk_fp8_f32 v245, v238, v239
	v_cvt_pk_fp8_f32 v242, v228, v229 op_sel:[0,0,1]
	v_cvt_pk_fp8_f32 v243, v232, v233 op_sel:[0,0,1]
	v_cvt_pk_fp8_f32 v244, v236, v237 op_sel:[0,0,1]
	v_cvt_pk_fp8_f32 v245, v240, v241 op_sel:[0,0,1]
	s_nop 0
	global_store_dwordx4 v91, v[242:245], s[6:7]
	ds_read_b32 v226, v213
	ds_read_b32 v227, v213 offset:512
	ds_read_b32 v228, v213 offset:1024
	ds_read_b32 v229, v213 offset:1536
	ds_read_b32 v230, v213 offset:2048
	ds_read_b32 v231, v213 offset:2560
	ds_read_b32 v232, v213 offset:3072
	ds_read_b32 v233, v213 offset:3584
	ds_read_b32 v234, v213 offset:4096
	ds_read_b32 v235, v213 offset:4608
	ds_read_b32 v236, v213 offset:5120
	ds_read_b32 v237, v213 offset:5632
	ds_read_b32 v238, v213 offset:6144
	ds_read_b32 v239, v213 offset:6656
	ds_read_b32 v240, v213 offset:7168
	ds_read_b32 v241, v213 offset:7680
	s_waitcnt lgkmcnt(0)
	v_max_f32_e32 v226, v226, v226
	v_max_f32_e32 v227, v227, v227
	v_max_f32_e32 v228, v228, v228
	v_max_f32_e32 v229, v229, v229
	v_max_f32_e32 v230, v230, v230
	v_max_f32_e32 v231, v231, v231
	v_max_f32_e32 v232, v232, v232
	v_max_f32_e32 v233, v233, v233
	v_max_f32_e32 v234, v234, v234
	v_max_f32_e32 v235, v235, v235
	v_max_f32_e32 v236, v236, v236
	v_max_f32_e32 v237, v237, v237
	v_max_f32_e32 v238, v238, v238
	v_max_f32_e32 v239, v239, v239
	v_max_f32_e32 v240, v240, v240
	v_max_f32_e32 v241, v241, v241
	v_med3_f32 v226, v226, s62, v95
	v_med3_f32 v227, v227, s62, v95
	v_med3_f32 v228, v228, s62, v95
	v_med3_f32 v229, v229, s62, v95
	v_med3_f32 v230, v230, s62, v95
	v_med3_f32 v231, v231, s62, v95
	v_med3_f32 v232, v232, s62, v95
	v_med3_f32 v233, v233, s62, v95
	v_med3_f32 v234, v234, s62, v95
	v_med3_f32 v235, v235, s62, v95
	v_med3_f32 v236, v236, s62, v95
	v_med3_f32 v237, v237, s62, v95
	v_med3_f32 v238, v238, s62, v95
	v_med3_f32 v239, v239, s62, v95
	v_med3_f32 v240, v240, s62, v95
	v_med3_f32 v241, v241, s62, v95
	v_mov_b32_e32 v242, 0
	v_mov_b32_e32 v243, 0
	v_mov_b32_e32 v244, 0
	v_mov_b32_e32 v245, 0
	v_cvt_pk_fp8_f32 v242, v226, v227
	v_cvt_pk_fp8_f32 v243, v230, v231
	v_cvt_pk_fp8_f32 v244, v234, v235
	v_cvt_pk_fp8_f32 v245, v238, v239
	v_cvt_pk_fp8_f32 v242, v228, v229 op_sel:[0,0,1]
	v_cvt_pk_fp8_f32 v243, v232, v233 op_sel:[0,0,1]
	v_cvt_pk_fp8_f32 v244, v236, v237 op_sel:[0,0,1]
	v_cvt_pk_fp8_f32 v245, v240, v241 op_sel:[0,0,1]
	s_nop 0
	global_store_dwordx4 v92, v[242:245], s[6:7]
	s_waitcnt vmcnt(12)
	v_mul_f32_e32 v176, v50, v176
	v_mul_f32_e32 v177, v50, v177
	v_mul_f32_e32 v178, v50, v178
	v_mul_f32_e32 v179, v50, v179
	ds_write_b128 v210, v[176:179]
	v_mul_f32_e32 v180, v51, v180
	v_mul_f32_e32 v181, v51, v181
	v_mul_f32_e32 v182, v51, v182
	v_mul_f32_e32 v183, v51, v183
	ds_write_b128 v210, v[180:183] offset:1024
	v_mul_f32_e32 v184, v52, v184
	v_mul_f32_e32 v185, v52, v185
	v_mul_f32_e32 v186, v52, v186
	v_mul_f32_e32 v187, v52, v187
	ds_write_b128 v210, v[184:187] offset:2048
	v_mul_f32_e32 v188, v53, v188
	v_mul_f32_e32 v189, v53, v189
	v_mul_f32_e32 v190, v53, v190
	v_mul_f32_e32 v191, v53, v191
	ds_write_b128 v210, v[188:191] offset:3072
	v_mul_f32_e32 v192, v54, v192
	v_mul_f32_e32 v193, v54, v193
	v_mul_f32_e32 v194, v54, v194
	v_mul_f32_e32 v195, v54, v195
	ds_write_b128 v210, v[192:195] offset:4096
	v_mul_f32_e32 v196, v55, v196
	v_mul_f32_e32 v197, v55, v197
	v_mul_f32_e32 v198, v55, v198
	v_mul_f32_e32 v199, v55, v199
	ds_write_b128 v210, v[196:199] offset:5120
	v_mul_f32_e32 v200, v56, v200
	v_mul_f32_e32 v201, v56, v201
	v_mul_f32_e32 v202, v56, v202
	v_mul_f32_e32 v203, v56, v203
	ds_write_b128 v210, v[200:203] offset:6144
	v_mul_f32_e32 v204, v57, v204
	v_mul_f32_e32 v205, v57, v205
	v_mul_f32_e32 v206, v57, v206
	v_mul_f32_e32 v207, v57, v207
	ds_write_b128 v210, v[204:207] offset:7168
	s_waitcnt lgkmcnt(0)
	s_barrier
; #define GAS __attribute__((address_space(1)))
; #define LAS __attribute__((address_space(3)))
; #define LDS_WAIT() asm volatile("s_waitcnt lgkmcnt(0)" ::: "memory")
; __device__ __forceinline__ int src_col_in(int c) {
;     if (c < 5120) { const int blk = c >> 7, p = c & 127; const bool rope = blk < 16 || ((((blk - 16) >> 2) & 1) == 0); const int d = rope ? (p >> 1) + 64 * (p & 1) : p; return blk * 128 + d; }
;     if (c < OFF_Z) return c + 2096;
;     if (c < OFF_G) return c - 4048;
;     if (c < OFF_DT) return 5120 + (c - OFF_G);
;     if (c < NSRC) return c;
;     return -1;
; }
;     const int pr = item >> 1, kb = 2 * (pr / nblk) + (item & 1), nb = pr % nblk, k0 = 64 * kb, n0 = 32 * nb;
;     const int nr = n0 + (lane & 31); const int sc = MAP == 1 ? src_col_in(nr) : nr;
;     float v[32];
; #pragma unroll
;     for (int i = 0; i < 32; ++i) v[i] = sc >= 0 ? W[(size_t)(k0 + 2 * i + (lane >> 5)) * Nsrc + sc] : 0.f;
; #pragma unroll
;     for (int i = 0; i < 32; ++i) { const int k = k0 + 2 * i + (lane >> 5); float x = v[i] * wscale; if (KS) x *= (k < ksplit ? ksA[k] : ksB[k - ksplit]); scr[(2 * i + (lane >> 5)) * 33 + (lane & 31)] = x; }
;     LDS_WAIT(); asm volatile("" ::: "memory");
;     const int c = lane & 7;
; #pragma unroll
;     for (int j = 0; j < 4; ++j) { const int n = (lane >> 3) + 8 * j; const LAS float* s = scr + (8 * c) * 33 + n;
;         const unsigned long long o = (unsigned long long)pg8::pk4_fp8(s[0 * 33], s[1 * 33], s[2 * 33], s[3 * 33]) | ((unsigned long long)pg8::pk4_fp8(s[4 * 33], s[5 * 33], s[6 * 33], s[7 * 33]) << 32);
;         *(GAS unsigned long long*)(WT + (size_t)(n0 + n) * K + k0 + 8 * c) = o; }
;     LDS_WAIT(); asm volatile("" ::: "memory");
; }
	s_add_i32 s24, s23, 32
	s_lshl_b32 s20, s24, 7
	s_cmp_lt_u32 s24, 40
	s_cselect_b32 s21, 0, 0x830
	s_cmp_lt_u32 s24, 72
	s_cselect_b32 s21, s21, 0xfffff030
	s_add_i32 s20, s20, s21
	s_lshl_b32 s20, s20, 2
	s_add_u32 s8, s50, s20
	s_addc_u32 s9, s51, 0
	global_load_dwordx4 v[176:179], v76, s[8:9]
	s_add_u32 s8, s8, 0x16280
	s_addc_u32 s9, s9, 0
	global_load_dwordx4 v[180:183], v76, s[8:9]
	s_add_u32 s8, s8, 0x16280
	s_addc_u32 s9, s9, 0
	global_load_dwordx4 v[184:187], v76, s[8:9]
	s_add_u32 s8, s8, 0x16280
	s_addc_u32 s9, s9, 0
	global_load_dwordx4 v[188:191], v76, s[8:9]
	s_add_u32 s8, s8, 0x16280
	s_addc_u32 s9, s9, 0
	global_load_dwordx4 v[192:195], v76, s[8:9]
	s_add_u32 s8, s8, 0x16280
	s_addc_u32 s9, s9, 0
	global_load_dwordx4 v[196:199], v76, s[8:9]
	s_add_u32 s8, s8, 0x16280
	s_addc_u32 s9, s9, 0
	global_load_dwordx4 v[200:203], v76, s[8:9]
	s_add_u32 s8, s8, 0x16280
	s_addc_u32 s9, s9, 0
	global_load_dwordx4 v[204:207], v76, s[8:9]
	s_add_i32 s24, s23, 16
	s_mul_i32 s20, s24, 0x80000
	s_add_u32 s6, s52, s20
	s_addc_u32 s7, s53, 0
	s_cmp_lt_u32 s24, 16
	s_cselect_b32 s20, 1, 0
	s_sub_i32 s21, s24, 16
	s_bitcmp0_b32 s21, 2
	s_cselect_b32 s21, 1, 0
	s_cmp_lt_u32 s24, 40
	s_cselect_b32 s21, s21, 0
	s_or_b32 s20, s20, s21
	s_cmp_lg_u32 s20, 0
	s_cselect_b64 s[20:21], -1, 0
	v_cndmask_b32_e64 v91, v77, v81, s[20:21]
	v_cndmask_b32_e64 v92, v78, v82, s[20:21]
	ds_read_b32 v226, v212
	ds_read_b32 v227, v212 offset:512
	ds_read_b32 v228, v212 offset:1024
	ds_read_b32 v229, v212 offset:1536
	ds_read_b32 v230, v212 offset:2048
	ds_read_b32 v231, v212 offset:2560
	ds_read_b32 v232, v212 offset:3072
	ds_read_b32 v233, v212 offset:3584
	ds_read_b32 v234, v212 offset:4096
	ds_read_b32 v235, v212 offset:4608
	ds_read_b32 v236, v212 offset:5120
	ds_read_b32 v237, v212 offset:5632
	ds_read_b32 v238, v212 offset:6144
	ds_read_b32 v239, v212 offset:6656
	ds_read_b32 v240, v212 offset:7168
	ds_read_b32 v241, v212 offset:7680
	s_waitcnt lgkmcnt(0)
	v_max_f32_e32 v226, v226, v226
	v_max_f32_e32 v227, v227, v227
	v_max_f32_e32 v228, v228, v228
	v_max_f32_e32 v229, v229, v229
	v_max_f32_e32 v230, v230, v230
	v_max_f32_e32 v231, v231, v231
	v_max_f32_e32 v232, v232, v232
	v_max_f32_e32 v233, v233, v233
	v_max_f32_e32 v234, v234, v234
	v_max_f32_e32 v235, v235, v235
	v_max_f32_e32 v236, v236, v236
	v_max_f32_e32 v237, v237, v237
	v_max_f32_e32 v238, v238, v238
	v_max_f32_e32 v239, v239, v239
	v_max_f32_e32 v240, v240, v240
	v_max_f32_e32 v241, v241, v241
	v_med3_f32 v226, v226, s62, v95
	v_med3_f32 v227, v227, s62, v95
	v_med3_f32 v228, v228, s62, v95
	v_med3_f32 v229, v229, s62, v95
	v_med3_f32 v230, v230, s62, v95
	v_med3_f32 v231, v231, s62, v95
	v_med3_f32 v232, v232, s62, v95
	v_med3_f32 v233, v233, s62, v95
	v_med3_f32 v234, v234, s62, v95
	v_med3_f32 v235, v235, s62, v95
	v_med3_f32 v236, v236, s62, v95
	v_med3_f32 v237, v237, s62, v95
	v_med3_f32 v238, v238, s62, v95
	v_med3_f32 v239, v239, s62, v95
	v_med3_f32 v240, v240, s62, v95
	v_med3_f32 v241, v241, s62, v95
	v_mov_b32_e32 v242, 0
	v_mov_b32_e32 v243, 0
	v_mov_b32_e32 v244, 0
	v_mov_b32_e32 v245, 0
	v_cvt_pk_fp8_f32 v242, v226, v227
	v_cvt_pk_fp8_f32 v243, v230, v231
	v_cvt_pk_fp8_f32 v244, v234, v235
	v_cvt_pk_fp8_f32 v245, v238, v239
	v_cvt_pk_fp8_f32 v242, v228, v229 op_sel:[0,0,1]
	v_cvt_pk_fp8_f32 v243, v232, v233 op_sel:[0,0,1]
	v_cvt_pk_fp8_f32 v244, v236, v237 op_sel:[0,0,1]
	v_cvt_pk_fp8_f32 v245, v240, v241 op_sel:[0,0,1]
	s_nop 0
	global_store_dwordx4 v91, v[242:245], s[6:7]
	ds_read_b32 v226, v214
	ds_read_b32 v227, v214 offset:512
	ds_read_b32 v228, v214 offset:1024
	ds_read_b32 v229, v214 offset:1536
	ds_read_b32 v230, v214 offset:2048
	ds_read_b32 v231, v214 offset:2560
	ds_read_b32 v232, v214 offset:3072
	ds_read_b32 v233, v214 offset:3584
	ds_read_b32 v234, v214 offset:4096
	ds_read_b32 v235, v214 offset:4608
	ds_read_b32 v236, v214 offset:5120
	ds_read_b32 v237, v214 offset:5632
	ds_read_b32 v238, v214 offset:6144
	ds_read_b32 v239, v214 offset:6656
	ds_read_b32 v240, v214 offset:7168
	ds_read_b32 v241, v214 offset:7680
	s_waitcnt lgkmcnt(0)
	v_max_f32_e32 v226, v226, v226
	v_max_f32_e32 v227, v227, v227
	v_max_f32_e32 v228, v228, v228
	v_max_f32_e32 v229, v229, v229
	v_max_f32_e32 v230, v230, v230
	v_max_f32_e32 v231, v231, v231
	v_max_f32_e32 v232, v232, v232
	v_max_f32_e32 v233, v233, v233
	v_max_f32_e32 v234, v234, v234
	v_max_f32_e32 v235, v235, v235
	v_max_f32_e32 v236, v236, v236
	v_max_f32_e32 v237, v237, v237
	v_max_f32_e32 v238, v238, v238
	v_max_f32_e32 v239, v239, v239
	v_max_f32_e32 v240, v240, v240
	v_max_f32_e32 v241, v241, v241
	v_med3_f32 v226, v226, s62, v95
	v_med3_f32 v227, v227, s62, v95
	v_med3_f32 v228, v228, s62, v95
	v_med3_f32 v229, v229, s62, v95
	v_med3_f32 v230, v230, s62, v95
	v_med3_f32 v231, v231, s62, v95
	v_med3_f32 v232, v232, s62, v95
	v_med3_f32 v233, v233, s62, v95
	v_med3_f32 v234, v234, s62, v95
	v_med3_f32 v235, v235, s62, v95
	v_med3_f32 v236, v236, s62, v95
	v_med3_f32 v237, v237, s62, v95
	v_med3_f32 v238, v238, s62, v95
	v_med3_f32 v239, v239, s62, v95
	v_med3_f32 v240, v240, s62, v95
	v_med3_f32 v241, v241, s62, v95
	v_mov_b32_e32 v242, 0
	v_mov_b32_e32 v243, 0
	v_mov_b32_e32 v244, 0
	v_mov_b32_e32 v245, 0
	v_cvt_pk_fp8_f32 v242, v226, v227
	v_cvt_pk_fp8_f32 v243, v230, v231
	v_cvt_pk_fp8_f32 v244, v234, v235
	v_cvt_pk_fp8_f32 v245, v238, v239
	v_cvt_pk_fp8_f32 v242, v228, v229 op_sel:[0,0,1]
	v_cvt_pk_fp8_f32 v243, v232, v233 op_sel:[0,0,1]
	v_cvt_pk_fp8_f32 v244, v236, v237 op_sel:[0,0,1]
	v_cvt_pk_fp8_f32 v245, v240, v241 op_sel:[0,0,1]
	s_nop 0
	global_store_dwordx4 v92, v[242:245], s[6:7]
	s_waitcnt vmcnt(12)
	v_mul_f32_e32 v144, v50, v144
	v_mul_f32_e32 v145, v50, v145
	v_mul_f32_e32 v146, v50, v146
	v_mul_f32_e32 v147, v50, v147
	ds_write_b128 v209, v[144:147]
	v_mul_f32_e32 v148, v51, v148
	v_mul_f32_e32 v149, v51, v149
	v_mul_f32_e32 v150, v51, v150
	v_mul_f32_e32 v151, v51, v151
	ds_write_b128 v209, v[148:151] offset:1024
	v_mul_f32_e32 v152, v52, v152
	v_mul_f32_e32 v153, v52, v153
	v_mul_f32_e32 v154, v52, v154
	v_mul_f32_e32 v155, v52, v155
	ds_write_b128 v209, v[152:155] offset:2048
	v_mul_f32_e32 v156, v53, v156
	v_mul_f32_e32 v157, v53, v157
	v_mul_f32_e32 v158, v53, v158
	v_mul_f32_e32 v159, v53, v159
	ds_write_b128 v209, v[156:159] offset:3072
	v_mul_f32_e32 v160, v54, v160
	v_mul_f32_e32 v161, v54, v161
	v_mul_f32_e32 v162, v54, v162
	v_mul_f32_e32 v163, v54, v163
	ds_write_b128 v209, v[160:163] offset:4096
	v_mul_f32_e32 v164, v55, v164
	v_mul_f32_e32 v165, v55, v165
	v_mul_f32_e32 v166, v55, v166
	v_mul_f32_e32 v167, v55, v167
	ds_write_b128 v209, v[164:167] offset:5120
	v_mul_f32_e32 v168, v56, v168
	v_mul_f32_e32 v169, v56, v169
	v_mul_f32_e32 v170, v56, v170
	v_mul_f32_e32 v171, v56, v171
	ds_write_b128 v209, v[168:171] offset:6144
	v_mul_f32_e32 v172, v57, v172
	v_mul_f32_e32 v173, v57, v173
	v_mul_f32_e32 v174, v57, v174
	v_mul_f32_e32 v175, v57, v175
	ds_write_b128 v209, v[172:175] offset:7168
	s_waitcnt lgkmcnt(0)
	s_barrier
; #define GAS __attribute__((address_space(1)))
; #define LAS __attribute__((address_space(3)))
; #define LDS_WAIT() asm volatile("s_waitcnt lgkmcnt(0)" ::: "memory")
; __device__ __forceinline__ int src_col_in(int c) {
;     if (c < 5120) { const int blk = c >> 7, p = c & 127; const bool rope = blk < 16 || ((((blk - 16) >> 2) & 1) == 0); const int d = rope ? (p >> 1) + 64 * (p & 1) : p; return blk * 128 + d; }
;     if (c < OFF_Z) return c + 2096;
;     if (c < OFF_G) return c - 4048;
;     if (c < OFF_DT) return 5120 + (c - OFF_G);
;     const int pr = item >> 1, kb = 2 * (pr / nblk) + (item & 1), nb = pr % nblk, k0 = 64 * kb, n0 = 32 * nb;
;     const int nr = n0 + (lane & 31); const int sc = MAP == 1 ? src_col_in(nr) : nr;
;     float v[32];
; #pragma unroll
;     for (int i = 0; i < 32; ++i) v[i] = sc >= 0 ? W[(size_t)(k0 + 2 * i + (lane >> 5)) * Nsrc + sc] : 0.f;
; #pragma unroll
;     for (int i = 0; i < 32; ++i) { const int k = k0 + 2 * i + (lane >> 5); float x = v[i] * wscale; if (KS) x *= (k < ksplit ? ksA[k] : ksB[k - ksplit]); scr[(2 * i + (lane >> 5)) * 33 + (lane & 31)] = x; }
;     LDS_WAIT(); asm volatile("" ::: "memory");
;     const int c = lane & 7;
; #pragma unroll
;     for (int j = 0; j < 4; ++j) { const int n = (lane >> 3) + 8 * j; const LAS float* s = scr + (8 * c) * 33 + n;
;         const unsigned long long o = (unsigned long long)pg8::pk4_fp8(s[0 * 33], s[1 * 33], s[2 * 33], s[3 * 33]) | ((unsigned long long)pg8::pk4_fp8(s[4 * 33], s[5 * 33], s[6 * 33], s[7 * 33]) << 32);
;         *(GAS unsigned long long*)(WT + (size_t)(n0 + n) * K + k0 + 8 * c) = o; }
;     LDS_WAIT(); asm volatile("" ::: "memory");
	s_add_i32 s24, s23, 40
	s_lshl_b32 s20, s24, 7
	s_cmp_lt_u32 s24, 40
	s_cselect_b32 s21, 0, 0x830
	s_cmp_lt_u32 s24, 72
	s_cselect_b32 s21, s21, 0xfffff030
	s_add_i32 s20, s20, s21
	s_lshl_b32 s20, s20, 2
	s_add_u32 s8, s50, s20
	s_addc_u32 s9, s51, 0
	global_load_dwordx4 v[144:147], v76, s[8:9]
	s_add_u32 s8, s8, 0x16280
	s_addc_u32 s9, s9, 0
	global_load_dwordx4 v[148:151], v76, s[8:9]
	s_add_u32 s8, s8, 0x16280
	s_addc_u32 s9, s9, 0
	global_load_dwordx4 v[152:155], v76, s[8:9]
	s_add_u32 s8, s8, 0x16280
	s_addc_u32 s9, s9, 0
	global_load_dwordx4 v[156:159], v76, s[8:9]
	s_add_u32 s8, s8, 0x16280
	s_addc_u32 s9, s9, 0
	global_load_dwordx4 v[160:163], v76, s[8:9]
	s_add_u32 s8, s8, 0x16280
	s_addc_u32 s9, s9, 0
	global_load_dwordx4 v[164:167], v76, s[8:9]
	s_add_u32 s8, s8, 0x16280
	s_addc_u32 s9, s9, 0
	global_load_dwordx4 v[168:171], v76, s[8:9]
	s_add_u32 s8, s8, 0x16280
	s_addc_u32 s9, s9, 0
	global_load_dwordx4 v[172:175], v76, s[8:9]
	s_add_i32 s24, s23, 24
	s_mul_i32 s20, s24, 0x80000
	s_add_u32 s6, s52, s20
	s_addc_u32 s7, s53, 0
	s_cmp_lt_u32 s24, 16
	s_cselect_b32 s20, 1, 0
	s_sub_i32 s21, s24, 16
	s_bitcmp0_b32 s21, 2
	s_cselect_b32 s21, 1, 0
	s_cmp_lt_u32 s24, 40
	s_cselect_b32 s21, s21, 0
	s_or_b32 s20, s20, s21
	s_cmp_lg_u32 s20, 0
	s_cselect_b64 s[20:21], -1, 0
	v_cndmask_b32_e64 v91, v77, v81, s[20:21]
	v_cndmask_b32_e64 v92, v78, v82, s[20:21]
	ds_read_b32 v226, v211
	ds_read_b32 v227, v211 offset:512
	ds_read_b32 v228, v211 offset:1024
	ds_read_b32 v229, v211 offset:1536
	ds_read_b32 v230, v211 offset:2048
	ds_read_b32 v231, v211 offset:2560
	ds_read_b32 v232, v211 offset:3072
	ds_read_b32 v233, v211 offset:3584
	ds_read_b32 v234, v211 offset:4096
	ds_read_b32 v235, v211 offset:4608
	ds_read_b32 v236, v211 offset:5120
	ds_read_b32 v237, v211 offset:5632
	ds_read_b32 v238, v211 offset:6144
	ds_read_b32 v239, v211 offset:6656
	ds_read_b32 v240, v211 offset:7168
	ds_read_b32 v241, v211 offset:7680
	s_waitcnt lgkmcnt(0)
	v_max_f32_e32 v226, v226, v226
	v_max_f32_e32 v227, v227, v227
	v_max_f32_e32 v228, v228, v228
	v_max_f32_e32 v229, v229, v229
	v_max_f32_e32 v230, v230, v230
	v_max_f32_e32 v231, v231, v231
	v_max_f32_e32 v232, v232, v232
	v_max_f32_e32 v233, v233, v233
	v_max_f32_e32 v234, v234, v234
	v_max_f32_e32 v235, v235, v235
	v_max_f32_e32 v236, v236, v236
	v_max_f32_e32 v237, v237, v237
	v_max_f32_e32 v238, v238, v238
	v_max_f32_e32 v239, v239, v239
	v_max_f32_e32 v240, v240, v240
	v_max_f32_e32 v241, v241, v241
	v_med3_f32 v226, v226, s62, v95
	v_med3_f32 v227, v227, s62, v95
	v_med3_f32 v228, v228, s62, v95
	v_med3_f32 v229, v229, s62, v95
	v_med3_f32 v230, v230, s62, v95
	v_med3_f32 v231, v231, s62, v95
	v_med3_f32 v232, v232, s62, v95
	v_med3_f32 v233, v233, s62, v95
	v_med3_f32 v234, v234, s62, v95
	v_med3_f32 v235, v235, s62, v95
	v_med3_f32 v236, v236, s62, v95
	v_med3_f32 v237, v237, s62, v95
	v_med3_f32 v238, v238, s62, v95
	v_med3_f32 v239, v239, s62, v95
	v_med3_f32 v240, v240, s62, v95
	v_med3_f32 v241, v241, s62, v95
	v_mov_b32_e32 v242, 0
	v_mov_b32_e32 v243, 0
	v_mov_b32_e32 v244, 0
	v_mov_b32_e32 v245, 0
	v_cvt_pk_fp8_f32 v242, v226, v227
	v_cvt_pk_fp8_f32 v243, v230, v231
	v_cvt_pk_fp8_f32 v244, v234, v235
	v_cvt_pk_fp8_f32 v245, v238, v239
	v_cvt_pk_fp8_f32 v242, v228, v229 op_sel:[0,0,1]
	v_cvt_pk_fp8_f32 v243, v232, v233 op_sel:[0,0,1]
	v_cvt_pk_fp8_f32 v244, v236, v237 op_sel:[0,0,1]
	v_cvt_pk_fp8_f32 v245, v240, v241 op_sel:[0,0,1]
	s_nop 0
	global_store_dwordx4 v91, v[242:245], s[6:7]
	ds_read_b32 v226, v213
	ds_read_b32 v227, v213 offset:512
	ds_read_b32 v228, v213 offset:1024
	ds_read_b32 v229, v213 offset:1536
	ds_read_b32 v230, v213 offset:2048
	ds_read_b32 v231, v213 offset:2560
	ds_read_b32 v232, v213 offset:3072
	ds_read_b32 v233, v213 offset:3584
	ds_read_b32 v234, v213 offset:4096
	ds_read_b32 v235, v213 offset:4608
	ds_read_b32 v236, v213 offset:5120
	ds_read_b32 v237, v213 offset:5632
	ds_read_b32 v238, v213 offset:6144
	ds_read_b32 v239, v213 offset:6656
	ds_read_b32 v240, v213 offset:7168
	ds_read_b32 v241, v213 offset:7680
	s_waitcnt lgkmcnt(0)
	v_max_f32_e32 v226, v226, v226
	v_max_f32_e32 v227, v227, v227
	v_max_f32_e32 v228, v228, v228
	v_max_f32_e32 v229, v229, v229
	v_max_f32_e32 v230, v230, v230
	v_max_f32_e32 v231, v231, v231
	v_max_f32_e32 v232, v232, v232
	v_max_f32_e32 v233, v233, v233
	v_max_f32_e32 v234, v234, v234
	v_max_f32_e32 v235, v235, v235
	v_max_f32_e32 v236, v236, v236
	v_max_f32_e32 v237, v237, v237
	v_max_f32_e32 v238, v238, v238
	v_max_f32_e32 v239, v239, v239
	v_max_f32_e32 v240, v240, v240
	v_max_f32_e32 v241, v241, v241
	v_med3_f32 v226, v226, s62, v95
	v_med3_f32 v227, v227, s62, v95
	v_med3_f32 v228, v228, s62, v95
	v_med3_f32 v229, v229, s62, v95
	v_med3_f32 v230, v230, s62, v95
	v_med3_f32 v231, v231, s62, v95
	v_med3_f32 v232, v232, s62, v95
	v_med3_f32 v233, v233, s62, v95
	v_med3_f32 v234, v234, s62, v95
	v_med3_f32 v235, v235, s62, v95
	v_med3_f32 v236, v236, s62, v95
	v_med3_f32 v237, v237, s62, v95
	v_med3_f32 v238, v238, s62, v95
	v_med3_f32 v239, v239, s62, v95
	v_med3_f32 v240, v240, s62, v95
	v_med3_f32 v241, v241, s62, v95
	v_mov_b32_e32 v242, 0
	v_mov_b32_e32 v243, 0
	v_mov_b32_e32 v244, 0
	v_mov_b32_e32 v245, 0
	v_cvt_pk_fp8_f32 v242, v226, v227
	v_cvt_pk_fp8_f32 v243, v230, v231
	v_cvt_pk_fp8_f32 v244, v234, v235
	v_cvt_pk_fp8_f32 v245, v238, v239
	v_cvt_pk_fp8_f32 v242, v228, v229 op_sel:[0,0,1]
	v_cvt_pk_fp8_f32 v243, v232, v233 op_sel:[0,0,1]
	v_cvt_pk_fp8_f32 v244, v236, v237 op_sel:[0,0,1]
	v_cvt_pk_fp8_f32 v245, v240, v241 op_sel:[0,0,1]
	s_nop 0
	global_store_dwordx4 v92, v[242:245], s[6:7]
	s_waitcnt vmcnt(12)
	v_mul_f32_e32 v176, v50, v176
	v_mul_f32_e32 v177, v50, v177
	v_mul_f32_e32 v178, v50, v178
	v_mul_f32_e32 v179, v50, v179
	ds_write_b128 v210, v[176:179]
	v_mul_f32_e32 v180, v51, v180
	v_mul_f32_e32 v181, v51, v181
	v_mul_f32_e32 v182, v51, v182
	v_mul_f32_e32 v183, v51, v183
	ds_write_b128 v210, v[180:183] offset:1024
	v_mul_f32_e32 v184, v52, v184
	v_mul_f32_e32 v185, v52, v185
	v_mul_f32_e32 v186, v52, v186
	v_mul_f32_e32 v187, v52, v187
	ds_write_b128 v210, v[184:187] offset:2048
	v_mul_f32_e32 v188, v53, v188
	v_mul_f32_e32 v189, v53, v189
	v_mul_f32_e32 v190, v53, v190
	v_mul_f32_e32 v191, v53, v191
	ds_write_b128 v210, v[188:191] offset:3072
	v_mul_f32_e32 v192, v54, v192
	v_mul_f32_e32 v193, v54, v193
	v_mul_f32_e32 v194, v54, v194
	v_mul_f32_e32 v195, v54, v195
	ds_write_b128 v210, v[192:195] offset:4096
	v_mul_f32_e32 v196, v55, v196
	v_mul_f32_e32 v197, v55, v197
	v_mul_f32_e32 v198, v55, v198
	v_mul_f32_e32 v199, v55, v199
	ds_write_b128 v210, v[196:199] offset:5120
	v_mul_f32_e32 v200, v56, v200
	v_mul_f32_e32 v201, v56, v201
	v_mul_f32_e32 v202, v56, v202
	v_mul_f32_e32 v203, v56, v203
	ds_write_b128 v210, v[200:203] offset:6144
	v_mul_f32_e32 v204, v57, v204
	v_mul_f32_e32 v205, v57, v205
	v_mul_f32_e32 v206, v57, v206
	v_mul_f32_e32 v207, v57, v207
	ds_write_b128 v210, v[204:207] offset:7168
	s_waitcnt lgkmcnt(0)
	s_barrier
; #define GAS __attribute__((address_space(1)))
; #define LAS __attribute__((address_space(3)))
; #define LDS_WAIT() asm volatile("s_waitcnt lgkmcnt(0)" ::: "memory")
; __device__ __forceinline__ int src_col_in(int c) {
;     if (c < 5120) { const int blk = c >> 7, p = c & 127; const bool rope = blk < 16 || ((((blk - 16) >> 2) & 1) == 0); const int d = rope ? (p >> 1) + 64 * (p & 1) : p; return blk * 128 + d; }
;     if (c < OFF_Z) return c + 2096;
;     if (c < OFF_G) return c - 4048;
;     if (c < OFF_DT) return 5120 + (c - OFF_G);
;     const int pr = item >> 1, kb = 2 * (pr / nblk) + (item & 1), nb = pr % nblk, k0 = 64 * kb, n0 = 32 * nb;
;     const int nr = n0 + (lane & 31); const int sc = MAP == 1 ? src_col_in(nr) : nr;
;     float v[32];
; #pragma unroll
;     for (int i = 0; i < 32; ++i) v[i] = sc >= 0 ? W[(size_t)(k0 + 2 * i + (lane >> 5)) * Nsrc + sc] : 0.f;
; #pragma unroll
;     for (int i = 0; i < 32; ++i) { const int k = k0 + 2 * i + (lane >> 5); float x = v[i] * wscale; if (KS) x *= (k < ksplit ? ksA[k] : ksB[k - ksplit]); scr[(2 * i + (lane >> 5)) * 33 + (lane & 31)] = x; }
;     LDS_WAIT(); asm volatile("" ::: "memory");
;     const int c = lane & 7;
; #pragma unroll
;     for (int j = 0; j < 4; ++j) { const int n = (lane >> 3) + 8 * j; const LAS float* s = scr + (8 * c) * 33 + n;
;         const unsigned long long o = (unsigned long long)pg8::pk4_fp8(s[0 * 33], s[1 * 33], s[2 * 33], s[3 * 33]) | ((unsigned long long)pg8::pk4_fp8(s[4 * 33], s[5 * 33], s[6 * 33], s[7 * 33]) << 32);
;         *(GAS unsigned long long*)(WT + (size_t)(n0 + n) * K + k0 + 8 * c) = o; }
;     LDS_WAIT(); asm volatile("" ::: "memory");
	s_add_i32 s24, s23, 48
	s_lshl_b32 s20, s24, 7
	s_cmp_lt_u32 s24, 40
	s_cselect_b32 s21, 0, 0x830
	s_cmp_lt_u32 s24, 72
	s_cselect_b32 s21, s21, 0xfffff030
	s_add_i32 s20, s20, s21
	s_lshl_b32 s20, s20, 2
	s_add_u32 s8, s50, s20
	s_addc_u32 s9, s51, 0
	global_load_dwordx4 v[176:179], v76, s[8:9]
	s_add_u32 s8, s8, 0x16280
	s_addc_u32 s9, s9, 0
	global_load_dwordx4 v[180:183], v76, s[8:9]
	s_add_u32 s8, s8, 0x16280
	s_addc_u32 s9, s9, 0
	global_load_dwordx4 v[184:187], v76, s[8:9]
	s_add_u32 s8, s8, 0x16280
	s_addc_u32 s9, s9, 0
	global_load_dwordx4 v[188:191], v76, s[8:9]
	s_add_u32 s8, s8, 0x16280
	s_addc_u32 s9, s9, 0
	global_load_dwordx4 v[192:195], v76, s[8:9]
	s_add_u32 s8, s8, 0x16280
	s_addc_u32 s9, s9, 0
	global_load_dwordx4 v[196:199], v76, s[8:9]
	s_add_u32 s8, s8, 0x16280
	s_addc_u32 s9, s9, 0
	global_load_dwordx4 v[200:203], v76, s[8:9]
	s_add_u32 s8, s8, 0x16280
	s_addc_u32 s9, s9, 0
	global_load_dwordx4 v[204:207], v76, s[8:9]
	s_add_i32 s24, s23, 32
	s_mul_i32 s20, s24, 0x80000
	s_add_u32 s6, s52, s20
	s_addc_u32 s7, s53, 0
	s_cmp_lt_u32 s24, 16
	s_cselect_b32 s20, 1, 0
	s_sub_i32 s21, s24, 16
	s_bitcmp0_b32 s21, 2
	s_cselect_b32 s21, 1, 0
	s_cmp_lt_u32 s24, 40
	s_cselect_b32 s21, s21, 0
	s_or_b32 s20, s20, s21
	s_cmp_lg_u32 s20, 0
	s_cselect_b64 s[20:21], -1, 0
	v_cndmask_b32_e64 v91, v77, v81, s[20:21]
	v_cndmask_b32_e64 v92, v78, v82, s[20:21]
	ds_read_b32 v226, v212
	ds_read_b32 v227, v212 offset:512
	ds_read_b32 v228, v212 offset:1024
	ds_read_b32 v229, v212 offset:1536
	ds_read_b32 v230, v212 offset:2048
	ds_read_b32 v231, v212 offset:2560
	ds_read_b32 v232, v212 offset:3072
	ds_read_b32 v233, v212 offset:3584
	ds_read_b32 v234, v212 offset:4096
	ds_read_b32 v235, v212 offset:4608
	ds_read_b32 v236, v212 offset:5120
	ds_read_b32 v237, v212 offset:5632
	ds_read_b32 v238, v212 offset:6144
	ds_read_b32 v239, v212 offset:6656
	ds_read_b32 v240, v212 offset:7168
	ds_read_b32 v241, v212 offset:7680
	s_waitcnt lgkmcnt(0)
	v_max_f32_e32 v226, v226, v226
	v_max_f32_e32 v227, v227, v227
	v_max_f32_e32 v228, v228, v228
	v_max_f32_e32 v229, v229, v229
	v_max_f32_e32 v230, v230, v230
	v_max_f32_e32 v231, v231, v231
	v_max_f32_e32 v232, v232, v232
	v_max_f32_e32 v233, v233, v233
	v_max_f32_e32 v234, v234, v234
	v_max_f32_e32 v235, v235, v235
	v_max_f32_e32 v236, v236, v236
	v_max_f32_e32 v237, v237, v237
	v_max_f32_e32 v238, v238, v238
	v_max_f32_e32 v239, v239, v239
	v_max_f32_e32 v240, v240, v240
	v_max_f32_e32 v241, v241, v241
	v_med3_f32 v226, v226, s62, v95
	v_med3_f32 v227, v227, s62, v95
	v_med3_f32 v228, v228, s62, v95
	v_med3_f32 v229, v229, s62, v95
	v_med3_f32 v230, v230, s62, v95
	v_med3_f32 v231, v231, s62, v95
	v_med3_f32 v232, v232, s62, v95
	v_med3_f32 v233, v233, s62, v95
	v_med3_f32 v234, v234, s62, v95
	v_med3_f32 v235, v235, s62, v95
	v_med3_f32 v236, v236, s62, v95
	v_med3_f32 v237, v237, s62, v95
	v_med3_f32 v238, v238, s62, v95
	v_med3_f32 v239, v239, s62, v95
	v_med3_f32 v240, v240, s62, v95
	v_med3_f32 v241, v241, s62, v95
	v_mov_b32_e32 v242, 0
	v_mov_b32_e32 v243, 0
	v_mov_b32_e32 v244, 0
	v_mov_b32_e32 v245, 0
	v_cvt_pk_fp8_f32 v242, v226, v227
	v_cvt_pk_fp8_f32 v243, v230, v231
	v_cvt_pk_fp8_f32 v244, v234, v235
	v_cvt_pk_fp8_f32 v245, v238, v239
	v_cvt_pk_fp8_f32 v242, v228, v229 op_sel:[0,0,1]
	v_cvt_pk_fp8_f32 v243, v232, v233 op_sel:[0,0,1]
	v_cvt_pk_fp8_f32 v244, v236, v237 op_sel:[0,0,1]
	v_cvt_pk_fp8_f32 v245, v240, v241 op_sel:[0,0,1]
	s_nop 0
	global_store_dwordx4 v91, v[242:245], s[6:7]
	ds_read_b32 v226, v214
	ds_read_b32 v227, v214 offset:512
	ds_read_b32 v228, v214 offset:1024
	ds_read_b32 v229, v214 offset:1536
	ds_read_b32 v230, v214 offset:2048
	ds_read_b32 v231, v214 offset:2560
	ds_read_b32 v232, v214 offset:3072
	ds_read_b32 v233, v214 offset:3584
	ds_read_b32 v234, v214 offset:4096
	ds_read_b32 v235, v214 offset:4608
	ds_read_b32 v236, v214 offset:5120
	ds_read_b32 v237, v214 offset:5632
	ds_read_b32 v238, v214 offset:6144
	ds_read_b32 v239, v214 offset:6656
	ds_read_b32 v240, v214 offset:7168
	ds_read_b32 v241, v214 offset:7680
	s_waitcnt lgkmcnt(0)
	v_max_f32_e32 v226, v226, v226
	v_max_f32_e32 v227, v227, v227
	v_max_f32_e32 v228, v228, v228
	v_max_f32_e32 v229, v229, v229
	v_max_f32_e32 v230, v230, v230
	v_max_f32_e32 v231, v231, v231
	v_max_f32_e32 v232, v232, v232
	v_max_f32_e32 v233, v233, v233
	v_max_f32_e32 v234, v234, v234
	v_max_f32_e32 v235, v235, v235
	v_max_f32_e32 v236, v236, v236
	v_max_f32_e32 v237, v237, v237
	v_max_f32_e32 v238, v238, v238
	v_max_f32_e32 v239, v239, v239
	v_max_f32_e32 v240, v240, v240
	v_max_f32_e32 v241, v241, v241
	v_med3_f32 v226, v226, s62, v95
	v_med3_f32 v227, v227, s62, v95
	v_med3_f32 v228, v228, s62, v95
	v_med3_f32 v229, v229, s62, v95
	v_med3_f32 v230, v230, s62, v95
	v_med3_f32 v231, v231, s62, v95
	v_med3_f32 v232, v232, s62, v95
	v_med3_f32 v233, v233, s62, v95
	v_med3_f32 v234, v234, s62, v95
	v_med3_f32 v235, v235, s62, v95
	v_med3_f32 v236, v236, s62, v95
	v_med3_f32 v237, v237, s62, v95
	v_med3_f32 v238, v238, s62, v95
	v_med3_f32 v239, v239, s62, v95
	v_med3_f32 v240, v240, s62, v95
	v_med3_f32 v241, v241, s62, v95
	v_mov_b32_e32 v242, 0
	v_mov_b32_e32 v243, 0
	v_mov_b32_e32 v244, 0
	v_mov_b32_e32 v245, 0
	v_cvt_pk_fp8_f32 v242, v226, v227
	v_cvt_pk_fp8_f32 v243, v230, v231
	v_cvt_pk_fp8_f32 v244, v234, v235
	v_cvt_pk_fp8_f32 v245, v238, v239
	v_cvt_pk_fp8_f32 v242, v228, v229 op_sel:[0,0,1]
	v_cvt_pk_fp8_f32 v243, v232, v233 op_sel:[0,0,1]
	v_cvt_pk_fp8_f32 v244, v236, v237 op_sel:[0,0,1]
	v_cvt_pk_fp8_f32 v245, v240, v241 op_sel:[0,0,1]
	s_nop 0
	global_store_dwordx4 v92, v[242:245], s[6:7]
	s_waitcnt vmcnt(12)
	v_mul_f32_e32 v144, v50, v144
	v_mul_f32_e32 v145, v50, v145
	v_mul_f32_e32 v146, v50, v146
	v_mul_f32_e32 v147, v50, v147
	ds_write_b128 v209, v[144:147]
	v_mul_f32_e32 v148, v51, v148
	v_mul_f32_e32 v149, v51, v149
	v_mul_f32_e32 v150, v51, v150
	v_mul_f32_e32 v151, v51, v151
	ds_write_b128 v209, v[148:151] offset:1024
	v_mul_f32_e32 v152, v52, v152
	v_mul_f32_e32 v153, v52, v153
	v_mul_f32_e32 v154, v52, v154
	v_mul_f32_e32 v155, v52, v155
	ds_write_b128 v209, v[152:155] offset:2048
	v_mul_f32_e32 v156, v53, v156
	v_mul_f32_e32 v157, v53, v157
	v_mul_f32_e32 v158, v53, v158
	v_mul_f32_e32 v159, v53, v159
	ds_write_b128 v209, v[156:159] offset:3072
	v_mul_f32_e32 v160, v54, v160
	v_mul_f32_e32 v161, v54, v161
	v_mul_f32_e32 v162, v54, v162
	v_mul_f32_e32 v163, v54, v163
	ds_write_b128 v209, v[160:163] offset:4096
	v_mul_f32_e32 v164, v55, v164
	v_mul_f32_e32 v165, v55, v165
	v_mul_f32_e32 v166, v55, v166
	v_mul_f32_e32 v167, v55, v167
	ds_write_b128 v209, v[164:167] offset:5120
	v_mul_f32_e32 v168, v56, v168
	v_mul_f32_e32 v169, v56, v169
	v_mul_f32_e32 v170, v56, v170
	v_mul_f32_e32 v171, v56, v171
	ds_write_b128 v209, v[168:171] offset:6144
	v_mul_f32_e32 v172, v57, v172
	v_mul_f32_e32 v173, v57, v173
	v_mul_f32_e32 v174, v57, v174
	v_mul_f32_e32 v175, v57, v175
	ds_write_b128 v209, v[172:175] offset:7168
	s_waitcnt lgkmcnt(0)
	s_barrier
; #define GAS __attribute__((address_space(1)))
; #define LAS __attribute__((address_space(3)))
; #define LDS_WAIT() asm volatile("s_waitcnt lgkmcnt(0)" ::: "memory")
; __device__ __forceinline__ int src_col_in(int c) {
;     if (c < 5120) { const int blk = c >> 7, p = c & 127; const bool rope = blk < 16 || ((((blk - 16) >> 2) & 1) == 0); const int d = rope ? (p >> 1) + 64 * (p & 1) : p; return blk * 128 + d; }
;     if (c < OFF_Z) return c + 2096;
;     if (c < OFF_G) return c - 4048;
;     if (c < OFF_DT) return 5120 + (c - OFF_G);
;     const int pr = item >> 1, kb = 2 * (pr / nblk) + (item & 1), nb = pr % nblk, k0 = 64 * kb, n0 = 32 * nb;
;     const int nr = n0 + (lane & 31); const int sc = MAP == 1 ? src_col_in(nr) : nr;
;     float v[32];
; #pragma unroll
;     for (int i = 0; i < 32; ++i) v[i] = sc >= 0 ? W[(size_t)(k0 + 2 * i + (lane >> 5)) * Nsrc + sc] : 0.f;
; #pragma unroll
;     for (int i = 0; i < 32; ++i) { const int k = k0 + 2 * i + (lane >> 5); float x = v[i] * wscale; if (KS) x *= (k < ksplit ? ksA[k] : ksB[k - ksplit]); scr[(2 * i + (lane >> 5)) * 33 + (lane & 31)] = x; }
;     LDS_WAIT(); asm volatile("" ::: "memory");
;     const int c = lane & 7;
; #pragma unroll
;     for (int j = 0; j < 4; ++j) { const int n = (lane >> 3) + 8 * j; const LAS float* s = scr + (8 * c) * 33 + n;
;         const unsigned long long o = (unsigned long long)pg8::pk4_fp8(s[0 * 33], s[1 * 33], s[2 * 33], s[3 * 33]) | ((unsigned long long)pg8::pk4_fp8(s[4 * 33], s[5 * 33], s[6 * 33], s[7 * 33]) << 32);
;         *(GAS unsigned long long*)(WT + (size_t)(n0 + n) * K + k0 + 8 * c) = o; }
;     LDS_WAIT(); asm volatile("" ::: "memory");
	s_add_i32 s24, s23, 56
	s_lshl_b32 s20, s24, 7
	s_cmp_lt_u32 s24, 40
	s_cselect_b32 s21, 0, 0x830
	s_cmp_lt_u32 s24, 72
	s_cselect_b32 s21, s21, 0xfffff030
	s_add_i32 s20, s20, s21
	s_lshl_b32 s20, s20, 2
	s_add_u32 s8, s50, s20
	s_addc_u32 s9, s51, 0
	global_load_dwordx4 v[144:147], v76, s[8:9]
	s_add_u32 s8, s8, 0x16280
	s_addc_u32 s9, s9, 0
	global_load_dwordx4 v[148:151], v76, s[8:9]
	s_add_u32 s8, s8, 0x16280
	s_addc_u32 s9, s9, 0
	global_load_dwordx4 v[152:155], v76, s[8:9]
	s_add_u32 s8, s8, 0x16280
	s_addc_u32 s9, s9, 0
	global_load_dwordx4 v[156:159], v76, s[8:9]
	s_add_u32 s8, s8, 0x16280
	s_addc_u32 s9, s9, 0
	global_load_dwordx4 v[160:163], v76, s[8:9]
	s_add_u32 s8, s8, 0x16280
	s_addc_u32 s9, s9, 0
	global_load_dwordx4 v[164:167], v76, s[8:9]
	s_add_u32 s8, s8, 0x16280
	s_addc_u32 s9, s9, 0
	global_load_dwordx4 v[168:171], v76, s[8:9]
	s_add_u32 s8, s8, 0x16280
	s_addc_u32 s9, s9, 0
	global_load_dwordx4 v[172:175], v76, s[8:9]
	s_add_i32 s24, s23, 40
	s_mul_i32 s20, s24, 0x80000
	s_add_u32 s6, s52, s20
	s_addc_u32 s7, s53, 0
	s_cmp_lt_u32 s24, 16
	s_cselect_b32 s20, 1, 0
	s_sub_i32 s21, s24, 16
	s_bitcmp0_b32 s21, 2
	s_cselect_b32 s21, 1, 0
	s_cmp_lt_u32 s24, 40
	s_cselect_b32 s21, s21, 0
	s_or_b32 s20, s20, s21
	s_cmp_lg_u32 s20, 0
	s_cselect_b64 s[20:21], -1, 0
	v_cndmask_b32_e64 v91, v77, v81, s[20:21]
	v_cndmask_b32_e64 v92, v78, v82, s[20:21]
	ds_read_b32 v226, v211
	ds_read_b32 v227, v211 offset:512
	ds_read_b32 v228, v211 offset:1024
	ds_read_b32 v229, v211 offset:1536
	ds_read_b32 v230, v211 offset:2048
	ds_read_b32 v231, v211 offset:2560
	ds_read_b32 v232, v211 offset:3072
	ds_read_b32 v233, v211 offset:3584
	ds_read_b32 v234, v211 offset:4096
	ds_read_b32 v235, v211 offset:4608
	ds_read_b32 v236, v211 offset:5120
	ds_read_b32 v237, v211 offset:5632
	ds_read_b32 v238, v211 offset:6144
	ds_read_b32 v239, v211 offset:6656
	ds_read_b32 v240, v211 offset:7168
	ds_read_b32 v241, v211 offset:7680
	s_waitcnt lgkmcnt(0)
	v_max_f32_e32 v226, v226, v226
	v_max_f32_e32 v227, v227, v227
	v_max_f32_e32 v228, v228, v228
	v_max_f32_e32 v229, v229, v229
	v_max_f32_e32 v230, v230, v230
	v_max_f32_e32 v231, v231, v231
	v_max_f32_e32 v232, v232, v232
	v_max_f32_e32 v233, v233, v233
	v_max_f32_e32 v234, v234, v234
	v_max_f32_e32 v235, v235, v235
	v_max_f32_e32 v236, v236, v236
	v_max_f32_e32 v237, v237, v237
	v_max_f32_e32 v238, v238, v238
	v_max_f32_e32 v239, v239, v239
	v_max_f32_e32 v240, v240, v240
	v_max_f32_e32 v241, v241, v241
	v_med3_f32 v226, v226, s62, v95
	v_med3_f32 v227, v227, s62, v95
	v_med3_f32 v228, v228, s62, v95
	v_med3_f32 v229, v229, s62, v95
	v_med3_f32 v230, v230, s62, v95
	v_med3_f32 v231, v231, s62, v95
	v_med3_f32 v232, v232, s62, v95
	v_med3_f32 v233, v233, s62, v95
	v_med3_f32 v234, v234, s62, v95
	v_med3_f32 v235, v235, s62, v95
	v_med3_f32 v236, v236, s62, v95
	v_med3_f32 v237, v237, s62, v95
	v_med3_f32 v238, v238, s62, v95
	v_med3_f32 v239, v239, s62, v95
	v_med3_f32 v240, v240, s62, v95
	v_med3_f32 v241, v241, s62, v95
	v_mov_b32_e32 v242, 0
	v_mov_b32_e32 v243, 0
	v_mov_b32_e32 v244, 0
	v_mov_b32_e32 v245, 0
	v_cvt_pk_fp8_f32 v242, v226, v227
	v_cvt_pk_fp8_f32 v243, v230, v231
	v_cvt_pk_fp8_f32 v244, v234, v235
	v_cvt_pk_fp8_f32 v245, v238, v239
	v_cvt_pk_fp8_f32 v242, v228, v229 op_sel:[0,0,1]
	v_cvt_pk_fp8_f32 v243, v232, v233 op_sel:[0,0,1]
	v_cvt_pk_fp8_f32 v244, v236, v237 op_sel:[0,0,1]
	v_cvt_pk_fp8_f32 v245, v240, v241 op_sel:[0,0,1]
	s_nop 0
	global_store_dwordx4 v91, v[242:245], s[6:7]
	ds_read_b32 v226, v213
	ds_read_b32 v227, v213 offset:512
	ds_read_b32 v228, v213 offset:1024
	ds_read_b32 v229, v213 offset:1536
	ds_read_b32 v230, v213 offset:2048
	ds_read_b32 v231, v213 offset:2560
	ds_read_b32 v232, v213 offset:3072
	ds_read_b32 v233, v213 offset:3584
	ds_read_b32 v234, v213 offset:4096
	ds_read_b32 v235, v213 offset:4608
	ds_read_b32 v236, v213 offset:5120
	ds_read_b32 v237, v213 offset:5632
	ds_read_b32 v238, v213 offset:6144
	ds_read_b32 v239, v213 offset:6656
	ds_read_b32 v240, v213 offset:7168
	ds_read_b32 v241, v213 offset:7680
	s_waitcnt lgkmcnt(0)
	v_max_f32_e32 v226, v226, v226
	v_max_f32_e32 v227, v227, v227
	v_max_f32_e32 v228, v228, v228
	v_max_f32_e32 v229, v229, v229
	v_max_f32_e32 v230, v230, v230
	v_max_f32_e32 v231, v231, v231
	v_max_f32_e32 v232, v232, v232
	v_max_f32_e32 v233, v233, v233
	v_max_f32_e32 v234, v234, v234
	v_max_f32_e32 v235, v235, v235
	v_max_f32_e32 v236, v236, v236
	v_max_f32_e32 v237, v237, v237
	v_max_f32_e32 v238, v238, v238
	v_max_f32_e32 v239, v239, v239
	v_max_f32_e32 v240, v240, v240
	v_max_f32_e32 v241, v241, v241
	v_med3_f32 v226, v226, s62, v95
	v_med3_f32 v227, v227, s62, v95
	v_med3_f32 v228, v228, s62, v95
	v_med3_f32 v229, v229, s62, v95
	v_med3_f32 v230, v230, s62, v95
	v_med3_f32 v231, v231, s62, v95
	v_med3_f32 v232, v232, s62, v95
	v_med3_f32 v233, v233, s62, v95
	v_med3_f32 v234, v234, s62, v95
	v_med3_f32 v235, v235, s62, v95
	v_med3_f32 v236, v236, s62, v95
	v_med3_f32 v237, v237, s62, v95
	v_med3_f32 v238, v238, s62, v95
	v_med3_f32 v239, v239, s62, v95
	v_med3_f32 v240, v240, s62, v95
	v_med3_f32 v241, v241, s62, v95
	v_mov_b32_e32 v242, 0
	v_mov_b32_e32 v243, 0
	v_mov_b32_e32 v244, 0
	v_mov_b32_e32 v245, 0
	v_cvt_pk_fp8_f32 v242, v226, v227
	v_cvt_pk_fp8_f32 v243, v230, v231
	v_cvt_pk_fp8_f32 v244, v234, v235
	v_cvt_pk_fp8_f32 v245, v238, v239
	v_cvt_pk_fp8_f32 v242, v228, v229 op_sel:[0,0,1]
	v_cvt_pk_fp8_f32 v243, v232, v233 op_sel:[0,0,1]
	v_cvt_pk_fp8_f32 v244, v236, v237 op_sel:[0,0,1]
	v_cvt_pk_fp8_f32 v245, v240, v241 op_sel:[0,0,1]
	s_nop 0
	global_store_dwordx4 v92, v[242:245], s[6:7]
	s_waitcnt vmcnt(12)
	v_mul_f32_e32 v176, v50, v176
	v_mul_f32_e32 v177, v50, v177
	v_mul_f32_e32 v178, v50, v178
	v_mul_f32_e32 v179, v50, v179
	ds_write_b128 v210, v[176:179]
	v_mul_f32_e32 v180, v51, v180
	v_mul_f32_e32 v181, v51, v181
	v_mul_f32_e32 v182, v51, v182
	v_mul_f32_e32 v183, v51, v183
	ds_write_b128 v210, v[180:183] offset:1024
	v_mul_f32_e32 v184, v52, v184
	v_mul_f32_e32 v185, v52, v185
	v_mul_f32_e32 v186, v52, v186
	v_mul_f32_e32 v187, v52, v187
	ds_write_b128 v210, v[184:187] offset:2048
	v_mul_f32_e32 v188, v53, v188
	v_mul_f32_e32 v189, v53, v189
	v_mul_f32_e32 v190, v53, v190
	v_mul_f32_e32 v191, v53, v191
	ds_write_b128 v210, v[188:191] offset:3072
	v_mul_f32_e32 v192, v54, v192
	v_mul_f32_e32 v193, v54, v193
	v_mul_f32_e32 v194, v54, v194
	v_mul_f32_e32 v195, v54, v195
	ds_write_b128 v210, v[192:195] offset:4096
	v_mul_f32_e32 v196, v55, v196
	v_mul_f32_e32 v197, v55, v197
	v_mul_f32_e32 v198, v55, v198
	v_mul_f32_e32 v199, v55, v199
	ds_write_b128 v210, v[196:199] offset:5120
	v_mul_f32_e32 v200, v56, v200
	v_mul_f32_e32 v201, v56, v201
	v_mul_f32_e32 v202, v56, v202
	v_mul_f32_e32 v203, v56, v203
	ds_write_b128 v210, v[200:203] offset:6144
	v_mul_f32_e32 v204, v57, v204
	v_mul_f32_e32 v205, v57, v205
	v_mul_f32_e32 v206, v57, v206
	v_mul_f32_e32 v207, v57, v207
	ds_write_b128 v210, v[204:207] offset:7168
	s_waitcnt lgkmcnt(0)
	s_barrier
; #define GAS __attribute__((address_space(1)))
; #define LAS __attribute__((address_space(3)))
; #define LDS_WAIT() asm volatile("s_waitcnt lgkmcnt(0)" ::: "memory")
; __device__ __forceinline__ int src_col_in(int c) {
;     if (c < 5120) { const int blk = c >> 7, p = c & 127; const bool rope = blk < 16 || ((((blk - 16) >> 2) & 1) == 0); const int d = rope ? (p >> 1) + 64 * (p & 1) : p; return blk * 128 + d; }
;     if (c < OFF_Z) return c + 2096;
;     if (c < OFF_G) return c - 4048;
;     if (c < OFF_DT) return 5120 + (c - OFF_G);
;     const int pr = item >> 1, kb = 2 * (pr / nblk) + (item & 1), nb = pr % nblk, k0 = 64 * kb, n0 = 32 * nb;
;     const int nr = n0 + (lane & 31); const int sc = MAP == 1 ? src_col_in(nr) : nr;
;     float v[32];
; #pragma unroll
;     for (int i = 0; i < 32; ++i) v[i] = sc >= 0 ? W[(size_t)(k0 + 2 * i + (lane >> 5)) * Nsrc + sc] : 0.f;
; #pragma unroll
;     for (int i = 0; i < 32; ++i) { const int k = k0 + 2 * i + (lane >> 5); float x = v[i] * wscale; if (KS) x *= (k < ksplit ? ksA[k] : ksB[k - ksplit]); scr[(2 * i + (lane >> 5)) * 33 + (lane & 31)] = x; }
;     LDS_WAIT(); asm volatile("" ::: "memory");
;     const int c = lane & 7;
; #pragma unroll
;     for (int j = 0; j < 4; ++j) { const int n = (lane >> 3) + 8 * j; const LAS float* s = scr + (8 * c) * 33 + n;
;         const unsigned long long o = (unsigned long long)pg8::pk4_fp8(s[0 * 33], s[1 * 33], s[2 * 33], s[3 * 33]) | ((unsigned long long)pg8::pk4_fp8(s[4 * 33], s[5 * 33], s[6 * 33], s[7 * 33]) << 32);
;         *(GAS unsigned long long*)(WT + (size_t)(n0 + n) * K + k0 + 8 * c) = o; }
;     LDS_WAIT(); asm volatile("" ::: "memory");
	s_add_i32 s24, s23, 64
	s_lshl_b32 s20, s24, 7
	s_cmp_lt_u32 s24, 40
	s_cselect_b32 s21, 0, 0x830
	s_cmp_lt_u32 s24, 72
	s_cselect_b32 s21, s21, 0xfffff030
	s_add_i32 s20, s20, s21
	s_lshl_b32 s20, s20, 2
	s_add_u32 s8, s50, s20
	s_addc_u32 s9, s51, 0
	global_load_dwordx4 v[176:179], v76, s[8:9]
	s_add_u32 s8, s8, 0x16280
	s_addc_u32 s9, s9, 0
	global_load_dwordx4 v[180:183], v76, s[8:9]
	s_add_u32 s8, s8, 0x16280
	s_addc_u32 s9, s9, 0
	global_load_dwordx4 v[184:187], v76, s[8:9]
	s_add_u32 s8, s8, 0x16280
	s_addc_u32 s9, s9, 0
	global_load_dwordx4 v[188:191], v76, s[8:9]
	s_add_u32 s8, s8, 0x16280
	s_addc_u32 s9, s9, 0
	global_load_dwordx4 v[192:195], v76, s[8:9]
	s_add_u32 s8, s8, 0x16280
	s_addc_u32 s9, s9, 0
	global_load_dwordx4 v[196:199], v76, s[8:9]
	s_add_u32 s8, s8, 0x16280
	s_addc_u32 s9, s9, 0
	global_load_dwordx4 v[200:203], v76, s[8:9]
	s_add_u32 s8, s8, 0x16280
	s_addc_u32 s9, s9, 0
	global_load_dwordx4 v[204:207], v76, s[8:9]
	s_add_i32 s24, s23, 48
	s_mul_i32 s20, s24, 0x80000
	s_add_u32 s6, s52, s20
	s_addc_u32 s7, s53, 0
	s_cmp_lt_u32 s24, 16
	s_cselect_b32 s20, 1, 0
	s_sub_i32 s21, s24, 16
	s_bitcmp0_b32 s21, 2
	s_cselect_b32 s21, 1, 0
	s_cmp_lt_u32 s24, 40
	s_cselect_b32 s21, s21, 0
	s_or_b32 s20, s20, s21
	s_cmp_lg_u32 s20, 0
	s_cselect_b64 s[20:21], -1, 0
	v_cndmask_b32_e64 v91, v77, v81, s[20:21]
	v_cndmask_b32_e64 v92, v78, v82, s[20:21]
	ds_read_b32 v226, v212
	ds_read_b32 v227, v212 offset:512
	ds_read_b32 v228, v212 offset:1024
	ds_read_b32 v229, v212 offset:1536
	ds_read_b32 v230, v212 offset:2048
	ds_read_b32 v231, v212 offset:2560
	ds_read_b32 v232, v212 offset:3072
	ds_read_b32 v233, v212 offset:3584
	ds_read_b32 v234, v212 offset:4096
	ds_read_b32 v235, v212 offset:4608
	ds_read_b32 v236, v212 offset:5120
	ds_read_b32 v237, v212 offset:5632
	ds_read_b32 v238, v212 offset:6144
	ds_read_b32 v239, v212 offset:6656
	ds_read_b32 v240, v212 offset:7168
	ds_read_b32 v241, v212 offset:7680
	s_waitcnt lgkmcnt(0)
	v_max_f32_e32 v226, v226, v226
	v_max_f32_e32 v227, v227, v227
	v_max_f32_e32 v228, v228, v228
	v_max_f32_e32 v229, v229, v229
	v_max_f32_e32 v230, v230, v230
	v_max_f32_e32 v231, v231, v231
	v_max_f32_e32 v232, v232, v232
	v_max_f32_e32 v233, v233, v233
	v_max_f32_e32 v234, v234, v234
	v_max_f32_e32 v235, v235, v235
	v_max_f32_e32 v236, v236, v236
	v_max_f32_e32 v237, v237, v237
	v_max_f32_e32 v238, v238, v238
	v_max_f32_e32 v239, v239, v239
	v_max_f32_e32 v240, v240, v240
	v_max_f32_e32 v241, v241, v241
	v_med3_f32 v226, v226, s62, v95
	v_med3_f32 v227, v227, s62, v95
	v_med3_f32 v228, v228, s62, v95
	v_med3_f32 v229, v229, s62, v95
	v_med3_f32 v230, v230, s62, v95
	v_med3_f32 v231, v231, s62, v95
	v_med3_f32 v232, v232, s62, v95
	v_med3_f32 v233, v233, s62, v95
	v_med3_f32 v234, v234, s62, v95
	v_med3_f32 v235, v235, s62, v95
	v_med3_f32 v236, v236, s62, v95
	v_med3_f32 v237, v237, s62, v95
	v_med3_f32 v238, v238, s62, v95
	v_med3_f32 v239, v239, s62, v95
	v_med3_f32 v240, v240, s62, v95
	v_med3_f32 v241, v241, s62, v95
	v_mov_b32_e32 v242, 0
	v_mov_b32_e32 v243, 0
	v_mov_b32_e32 v244, 0
	v_mov_b32_e32 v245, 0
	v_cvt_pk_fp8_f32 v242, v226, v227
	v_cvt_pk_fp8_f32 v243, v230, v231
	v_cvt_pk_fp8_f32 v244, v234, v235
	v_cvt_pk_fp8_f32 v245, v238, v239
	v_cvt_pk_fp8_f32 v242, v228, v229 op_sel:[0,0,1]
	v_cvt_pk_fp8_f32 v243, v232, v233 op_sel:[0,0,1]
	v_cvt_pk_fp8_f32 v244, v236, v237 op_sel:[0,0,1]
	v_cvt_pk_fp8_f32 v245, v240, v241 op_sel:[0,0,1]
	s_nop 0
	global_store_dwordx4 v91, v[242:245], s[6:7]
	ds_read_b32 v226, v214
	ds_read_b32 v227, v214 offset:512
	ds_read_b32 v228, v214 offset:1024
	ds_read_b32 v229, v214 offset:1536
	ds_read_b32 v230, v214 offset:2048
	ds_read_b32 v231, v214 offset:2560
	ds_read_b32 v232, v214 offset:3072
	ds_read_b32 v233, v214 offset:3584
	ds_read_b32 v234, v214 offset:4096
	ds_read_b32 v235, v214 offset:4608
	ds_read_b32 v236, v214 offset:5120
	ds_read_b32 v237, v214 offset:5632
	ds_read_b32 v238, v214 offset:6144
	ds_read_b32 v239, v214 offset:6656
	ds_read_b32 v240, v214 offset:7168
	ds_read_b32 v241, v214 offset:7680
	s_waitcnt lgkmcnt(0)
	v_max_f32_e32 v226, v226, v226
	v_max_f32_e32 v227, v227, v227
	v_max_f32_e32 v228, v228, v228
	v_max_f32_e32 v229, v229, v229
	v_max_f32_e32 v230, v230, v230
	v_max_f32_e32 v231, v231, v231
	v_max_f32_e32 v232, v232, v232
	v_max_f32_e32 v233, v233, v233
	v_max_f32_e32 v234, v234, v234
	v_max_f32_e32 v235, v235, v235
	v_max_f32_e32 v236, v236, v236
	v_max_f32_e32 v237, v237, v237
	v_max_f32_e32 v238, v238, v238
	v_max_f32_e32 v239, v239, v239
	v_max_f32_e32 v240, v240, v240
	v_max_f32_e32 v241, v241, v241
	v_med3_f32 v226, v226, s62, v95
	v_med3_f32 v227, v227, s62, v95
	v_med3_f32 v228, v228, s62, v95
	v_med3_f32 v229, v229, s62, v95
	v_med3_f32 v230, v230, s62, v95
	v_med3_f32 v231, v231, s62, v95
	v_med3_f32 v232, v232, s62, v95
	v_med3_f32 v233, v233, s62, v95
	v_med3_f32 v234, v234, s62, v95
	v_med3_f32 v235, v235, s62, v95
	v_med3_f32 v236, v236, s62, v95
	v_med3_f32 v237, v237, s62, v95
	v_med3_f32 v238, v238, s62, v95
	v_med3_f32 v239, v239, s62, v95
	v_med3_f32 v240, v240, s62, v95
	v_med3_f32 v241, v241, s62, v95
	v_mov_b32_e32 v242, 0
	v_mov_b32_e32 v243, 0
	v_mov_b32_e32 v244, 0
	v_mov_b32_e32 v245, 0
	v_cvt_pk_fp8_f32 v242, v226, v227
	v_cvt_pk_fp8_f32 v243, v230, v231
	v_cvt_pk_fp8_f32 v244, v234, v235
	v_cvt_pk_fp8_f32 v245, v238, v239
	v_cvt_pk_fp8_f32 v242, v228, v229 op_sel:[0,0,1]
	v_cvt_pk_fp8_f32 v243, v232, v233 op_sel:[0,0,1]
	v_cvt_pk_fp8_f32 v244, v236, v237 op_sel:[0,0,1]
	v_cvt_pk_fp8_f32 v245, v240, v241 op_sel:[0,0,1]
	s_nop 0
	global_store_dwordx4 v92, v[242:245], s[6:7]
	s_waitcnt vmcnt(12)
	v_mul_f32_e32 v144, v50, v144
	v_mul_f32_e32 v145, v50, v145
	v_mul_f32_e32 v146, v50, v146
	v_mul_f32_e32 v147, v50, v147
	ds_write_b128 v209, v[144:147]
	v_mul_f32_e32 v148, v51, v148
	v_mul_f32_e32 v149, v51, v149
	v_mul_f32_e32 v150, v51, v150
	v_mul_f32_e32 v151, v51, v151
	ds_write_b128 v209, v[148:151] offset:1024
	v_mul_f32_e32 v152, v52, v152
	v_mul_f32_e32 v153, v52, v153
	v_mul_f32_e32 v154, v52, v154
	v_mul_f32_e32 v155, v52, v155
	ds_write_b128 v209, v[152:155] offset:2048
	v_mul_f32_e32 v156, v53, v156
	v_mul_f32_e32 v157, v53, v157
	v_mul_f32_e32 v158, v53, v158
	v_mul_f32_e32 v159, v53, v159
	ds_write_b128 v209, v[156:159] offset:3072
	v_mul_f32_e32 v160, v54, v160
	v_mul_f32_e32 v161, v54, v161
	v_mul_f32_e32 v162, v54, v162
	v_mul_f32_e32 v163, v54, v163
	ds_write_b128 v209, v[160:163] offset:4096
	v_mul_f32_e32 v164, v55, v164
	v_mul_f32_e32 v165, v55, v165
	v_mul_f32_e32 v166, v55, v166
	v_mul_f32_e32 v167, v55, v167
	ds_write_b128 v209, v[164:167] offset:5120
	v_mul_f32_e32 v168, v56, v168
	v_mul_f32_e32 v169, v56, v169
	v_mul_f32_e32 v170, v56, v170
	v_mul_f32_e32 v171, v56, v171
	ds_write_b128 v209, v[168:171] offset:6144
	v_mul_f32_e32 v172, v57, v172
	v_mul_f32_e32 v173, v57, v173
	v_mul_f32_e32 v174, v57, v174
	v_mul_f32_e32 v175, v57, v175
	ds_write_b128 v209, v[172:175] offset:7168
	s_waitcnt lgkmcnt(0)
	s_barrier
; #define GAS __attribute__((address_space(1)))
; #define LAS __attribute__((address_space(3)))
; #define LDS_WAIT() asm volatile("s_waitcnt lgkmcnt(0)" ::: "memory")
; __device__ __forceinline__ int src_col_in(int c) {
;     if (c < 5120) { const int blk = c >> 7, p = c & 127; const bool rope = blk < 16 || ((((blk - 16) >> 2) & 1) == 0); const int d = rope ? (p >> 1) + 64 * (p & 1) : p; return blk * 128 + d; }
;     if (c < OFF_Z) return c + 2096;
;     if (c < OFF_G) return c - 4048;
;     if (c < OFF_DT) return 5120 + (c - OFF_G);
;     const int pr = item >> 1, kb = 2 * (pr / nblk) + (item & 1), nb = pr % nblk, k0 = 64 * kb, n0 = 32 * nb;
;     const int nr = n0 + (lane & 31); const int sc = MAP == 1 ? src_col_in(nr) : nr;
;     float v[32];
; #pragma unroll
;     for (int i = 0; i < 32; ++i) v[i] = sc >= 0 ? W[(size_t)(k0 + 2 * i + (lane >> 5)) * Nsrc + sc] : 0.f;
; #pragma unroll
;     for (int i = 0; i < 32; ++i) { const int k = k0 + 2 * i + (lane >> 5); float x = v[i] * wscale; if (KS) x *= (k < ksplit ? ksA[k] : ksB[k - ksplit]); scr[(2 * i + (lane >> 5)) * 33 + (lane & 31)] = x; }
;     LDS_WAIT(); asm volatile("" ::: "memory");
;     const int c = lane & 7;
; #pragma unroll
;     for (int j = 0; j < 4; ++j) { const int n = (lane >> 3) + 8 * j; const LAS float* s = scr + (8 * c) * 33 + n;
;         const unsigned long long o = (unsigned long long)pg8::pk4_fp8(s[0 * 33], s[1 * 33], s[2 * 33], s[3 * 33]) | ((unsigned long long)pg8::pk4_fp8(s[4 * 33], s[5 * 33], s[6 * 33], s[7 * 33]) << 32);
;         *(GAS unsigned long long*)(WT + (size_t)(n0 + n) * K + k0 + 8 * c) = o; }
;     LDS_WAIT(); asm volatile("" ::: "memory");
	s_add_i32 s24, s23, 72
	s_lshl_b32 s20, s24, 7
	s_cmp_lt_u32 s24, 40
	s_cselect_b32 s21, 0, 0x830
	s_cmp_lt_u32 s24, 72
	s_cselect_b32 s21, s21, 0xfffff030
	s_add_i32 s20, s20, s21
	s_lshl_b32 s20, s20, 2
	s_add_u32 s8, s50, s20
	s_addc_u32 s9, s51, 0
	global_load_dwordx4 v[144:147], v76, s[8:9]
	s_add_u32 s8, s8, 0x16280
	s_addc_u32 s9, s9, 0
	global_load_dwordx4 v[148:151], v76, s[8:9]
	s_add_u32 s8, s8, 0x16280
	s_addc_u32 s9, s9, 0
	global_load_dwordx4 v[152:155], v76, s[8:9]
	s_add_u32 s8, s8, 0x16280
	s_addc_u32 s9, s9, 0
	global_load_dwordx4 v[156:159], v76, s[8:9]
	s_add_u32 s8, s8, 0x16280
	s_addc_u32 s9, s9, 0
	global_load_dwordx4 v[160:163], v76, s[8:9]
	s_add_u32 s8, s8, 0x16280
	s_addc_u32 s9, s9, 0
	global_load_dwordx4 v[164:167], v76, s[8:9]
	s_add_u32 s8, s8, 0x16280
	s_addc_u32 s9, s9, 0
	global_load_dwordx4 v[168:171], v76, s[8:9]
	s_add_u32 s8, s8, 0x16280
	s_addc_u32 s9, s9, 0
	global_load_dwordx4 v[172:175], v76, s[8:9]
	s_add_i32 s24, s23, 56
	s_mul_i32 s20, s24, 0x80000
	s_add_u32 s6, s52, s20
	s_addc_u32 s7, s53, 0
	s_cmp_lt_u32 s24, 16
	s_cselect_b32 s20, 1, 0
	s_sub_i32 s21, s24, 16
	s_bitcmp0_b32 s21, 2
	s_cselect_b32 s21, 1, 0
	s_cmp_lt_u32 s24, 40
	s_cselect_b32 s21, s21, 0
	s_or_b32 s20, s20, s21
	s_cmp_lg_u32 s20, 0
	s_cselect_b64 s[20:21], -1, 0
	v_cndmask_b32_e64 v91, v77, v81, s[20:21]
	v_cndmask_b32_e64 v92, v78, v82, s[20:21]
	ds_read_b32 v226, v211
	ds_read_b32 v227, v211 offset:512
	ds_read_b32 v228, v211 offset:1024
	ds_read_b32 v229, v211 offset:1536
	ds_read_b32 v230, v211 offset:2048
	ds_read_b32 v231, v211 offset:2560
	ds_read_b32 v232, v211 offset:3072
	ds_read_b32 v233, v211 offset:3584
	ds_read_b32 v234, v211 offset:4096
	ds_read_b32 v235, v211 offset:4608
	ds_read_b32 v236, v211 offset:5120
	ds_read_b32 v237, v211 offset:5632
	ds_read_b32 v238, v211 offset:6144
	ds_read_b32 v239, v211 offset:6656
	ds_read_b32 v240, v211 offset:7168
	ds_read_b32 v241, v211 offset:7680
	s_waitcnt lgkmcnt(0)
	v_max_f32_e32 v226, v226, v226
	v_max_f32_e32 v227, v227, v227
	v_max_f32_e32 v228, v228, v228
	v_max_f32_e32 v229, v229, v229
	v_max_f32_e32 v230, v230, v230
	v_max_f32_e32 v231, v231, v231
	v_max_f32_e32 v232, v232, v232
	v_max_f32_e32 v233, v233, v233
	v_max_f32_e32 v234, v234, v234
	v_max_f32_e32 v235, v235, v235
	v_max_f32_e32 v236, v236, v236
	v_max_f32_e32 v237, v237, v237
	v_max_f32_e32 v238, v238, v238
	v_max_f32_e32 v239, v239, v239
	v_max_f32_e32 v240, v240, v240
	v_max_f32_e32 v241, v241, v241
	v_med3_f32 v226, v226, s62, v95
	v_med3_f32 v227, v227, s62, v95
	v_med3_f32 v228, v228, s62, v95
	v_med3_f32 v229, v229, s62, v95
	v_med3_f32 v230, v230, s62, v95
	v_med3_f32 v231, v231, s62, v95
	v_med3_f32 v232, v232, s62, v95
	v_med3_f32 v233, v233, s62, v95
	v_med3_f32 v234, v234, s62, v95
	v_med3_f32 v235, v235, s62, v95
	v_med3_f32 v236, v236, s62, v95
	v_med3_f32 v237, v237, s62, v95
	v_med3_f32 v238, v238, s62, v95
	v_med3_f32 v239, v239, s62, v95
	v_med3_f32 v240, v240, s62, v95
	v_med3_f32 v241, v241, s62, v95
	v_mov_b32_e32 v242, 0
	v_mov_b32_e32 v243, 0
	v_mov_b32_e32 v244, 0
	v_mov_b32_e32 v245, 0
	v_cvt_pk_fp8_f32 v242, v226, v227
	v_cvt_pk_fp8_f32 v243, v230, v231
	v_cvt_pk_fp8_f32 v244, v234, v235
	v_cvt_pk_fp8_f32 v245, v238, v239
	v_cvt_pk_fp8_f32 v242, v228, v229 op_sel:[0,0,1]
	v_cvt_pk_fp8_f32 v243, v232, v233 op_sel:[0,0,1]
	v_cvt_pk_fp8_f32 v244, v236, v237 op_sel:[0,0,1]
	v_cvt_pk_fp8_f32 v245, v240, v241 op_sel:[0,0,1]
	s_nop 0
	global_store_dwordx4 v91, v[242:245], s[6:7]
	ds_read_b32 v226, v213
	ds_read_b32 v227, v213 offset:512
	ds_read_b32 v228, v213 offset:1024
	ds_read_b32 v229, v213 offset:1536
	ds_read_b32 v230, v213 offset:2048
	ds_read_b32 v231, v213 offset:2560
	ds_read_b32 v232, v213 offset:3072
	ds_read_b32 v233, v213 offset:3584
	ds_read_b32 v234, v213 offset:4096
	ds_read_b32 v235, v213 offset:4608
	ds_read_b32 v236, v213 offset:5120
	ds_read_b32 v237, v213 offset:5632
	ds_read_b32 v238, v213 offset:6144
	ds_read_b32 v239, v213 offset:6656
	ds_read_b32 v240, v213 offset:7168
	ds_read_b32 v241, v213 offset:7680
	s_waitcnt lgkmcnt(0)
	v_max_f32_e32 v226, v226, v226
	v_max_f32_e32 v227, v227, v227
	v_max_f32_e32 v228, v228, v228
	v_max_f32_e32 v229, v229, v229
	v_max_f32_e32 v230, v230, v230
	v_max_f32_e32 v231, v231, v231
	v_max_f32_e32 v232, v232, v232
	v_max_f32_e32 v233, v233, v233
	v_max_f32_e32 v234, v234, v234
	v_max_f32_e32 v235, v235, v235
	v_max_f32_e32 v236, v236, v236
	v_max_f32_e32 v237, v237, v237
	v_max_f32_e32 v238, v238, v238
	v_max_f32_e32 v239, v239, v239
	v_max_f32_e32 v240, v240, v240
	v_max_f32_e32 v241, v241, v241
	v_med3_f32 v226, v226, s62, v95
	v_med3_f32 v227, v227, s62, v95
	v_med3_f32 v228, v228, s62, v95
	v_med3_f32 v229, v229, s62, v95
	v_med3_f32 v230, v230, s62, v95
	v_med3_f32 v231, v231, s62, v95
	v_med3_f32 v232, v232, s62, v95
	v_med3_f32 v233, v233, s62, v95
	v_med3_f32 v234, v234, s62, v95
	v_med3_f32 v235, v235, s62, v95
	v_med3_f32 v236, v236, s62, v95
	v_med3_f32 v237, v237, s62, v95
	v_med3_f32 v238, v238, s62, v95
	v_med3_f32 v239, v239, s62, v95
	v_med3_f32 v240, v240, s62, v95
	v_med3_f32 v241, v241, s62, v95
	v_mov_b32_e32 v242, 0
	v_mov_b32_e32 v243, 0
	v_mov_b32_e32 v244, 0
	v_mov_b32_e32 v245, 0
	v_cvt_pk_fp8_f32 v242, v226, v227
	v_cvt_pk_fp8_f32 v243, v230, v231
	v_cvt_pk_fp8_f32 v244, v234, v235
	v_cvt_pk_fp8_f32 v245, v238, v239
	v_cvt_pk_fp8_f32 v242, v228, v229 op_sel:[0,0,1]
	v_cvt_pk_fp8_f32 v243, v232, v233 op_sel:[0,0,1]
	v_cvt_pk_fp8_f32 v244, v236, v237 op_sel:[0,0,1]
	v_cvt_pk_fp8_f32 v245, v240, v241 op_sel:[0,0,1]
	s_nop 0
	global_store_dwordx4 v92, v[242:245], s[6:7]
	s_waitcnt vmcnt(12)
	v_mul_f32_e32 v176, v50, v176
	v_mul_f32_e32 v177, v50, v177
	v_mul_f32_e32 v178, v50, v178
	v_mul_f32_e32 v179, v50, v179
	ds_write_b128 v210, v[176:179]
	v_mul_f32_e32 v180, v51, v180
	v_mul_f32_e32 v181, v51, v181
	v_mul_f32_e32 v182, v51, v182
	v_mul_f32_e32 v183, v51, v183
	ds_write_b128 v210, v[180:183] offset:1024
	v_mul_f32_e32 v184, v52, v184
	v_mul_f32_e32 v185, v52, v185
	v_mul_f32_e32 v186, v52, v186
	v_mul_f32_e32 v187, v52, v187
	ds_write_b128 v210, v[184:187] offset:2048
	v_mul_f32_e32 v188, v53, v188
	v_mul_f32_e32 v189, v53, v189
	v_mul_f32_e32 v190, v53, v190
	v_mul_f32_e32 v191, v53, v191
	ds_write_b128 v210, v[188:191] offset:3072
	v_mul_f32_e32 v192, v54, v192
	v_mul_f32_e32 v193, v54, v193
	v_mul_f32_e32 v194, v54, v194
	v_mul_f32_e32 v195, v54, v195
	ds_write_b128 v210, v[192:195] offset:4096
	v_mul_f32_e32 v196, v55, v196
	v_mul_f32_e32 v197, v55, v197
	v_mul_f32_e32 v198, v55, v198
	v_mul_f32_e32 v199, v55, v199
	ds_write_b128 v210, v[196:199] offset:5120
	v_mul_f32_e32 v200, v56, v200
	v_mul_f32_e32 v201, v56, v201
	v_mul_f32_e32 v202, v56, v202
	v_mul_f32_e32 v203, v56, v203
	ds_write_b128 v210, v[200:203] offset:6144
	v_mul_f32_e32 v204, v57, v204
	v_mul_f32_e32 v205, v57, v205
	v_mul_f32_e32 v206, v57, v206
	v_mul_f32_e32 v207, v57, v207
	ds_write_b128 v210, v[204:207] offset:7168
	s_waitcnt lgkmcnt(0)
	s_barrier
; #define GAS __attribute__((address_space(1)))
; #define LAS __attribute__((address_space(3)))
; #define LDS_WAIT() asm volatile("s_waitcnt lgkmcnt(0)" ::: "memory")
; __device__ __forceinline__ int src_col_in(int c) {
;     if (c < 5120) { const int blk = c >> 7, p = c & 127; const bool rope = blk < 16 || ((((blk - 16) >> 2) & 1) == 0); const int d = rope ? (p >> 1) + 64 * (p & 1) : p; return blk * 128 + d; }
;     if (c < OFF_Z) return c + 2096;
;     if (c < OFF_G) return c - 4048;
;     if (c < OFF_DT) return 5120 + (c - OFF_G);
;     const int pr = item >> 1, kb = 2 * (pr / nblk) + (item & 1), nb = pr % nblk, k0 = 64 * kb, n0 = 32 * nb;
;     const int nr = n0 + (lane & 31); const int sc = MAP == 1 ? src_col_in(nr) : nr;
;     float v[32];
; #pragma unroll
;     for (int i = 0; i < 32; ++i) v[i] = sc >= 0 ? W[(size_t)(k0 + 2 * i + (lane >> 5)) * Nsrc + sc] : 0.f;
; #pragma unroll
;     for (int i = 0; i < 32; ++i) { const int k = k0 + 2 * i + (lane >> 5); float x = v[i] * wscale; if (KS) x *= (k < ksplit ? ksA[k] : ksB[k - ksplit]); scr[(2 * i + (lane >> 5)) * 33 + (lane & 31)] = x; }
;     LDS_WAIT(); asm volatile("" ::: "memory");
;     const int c = lane & 7;
; #pragma unroll
;     for (int j = 0; j < 4; ++j) { const int n = (lane >> 3) + 8 * j; const LAS float* s = scr + (8 * c) * 33 + n;
;         const unsigned long long o = (unsigned long long)pg8::pk4_fp8(s[0 * 33], s[1 * 33], s[2 * 33], s[3 * 33]) | ((unsigned long long)pg8::pk4_fp8(s[4 * 33], s[5 * 33], s[6 * 33], s[7 * 33]) << 32);
;         *(GAS unsigned long long*)(WT + (size_t)(n0 + n) * K + k0 + 8 * c) = o; }
;     LDS_WAIT(); asm volatile("" ::: "memory");
	s_add_i32 s24, s23, 80
	s_lshl_b32 s20, s24, 7
	s_cmp_lt_u32 s24, 40
	s_cselect_b32 s21, 0, 0x830
	s_cmp_lt_u32 s24, 72
	s_cselect_b32 s21, s21, 0xfffff030
	s_add_i32 s20, s20, s21
	s_lshl_b32 s20, s20, 2
	s_add_u32 s8, s50, s20
	s_addc_u32 s9, s51, 0
	global_load_dwordx4 v[176:179], v76, s[8:9]
	s_add_u32 s8, s8, 0x16280
	s_addc_u32 s9, s9, 0
	global_load_dwordx4 v[180:183], v76, s[8:9]
	s_add_u32 s8, s8, 0x16280
	s_addc_u32 s9, s9, 0
	global_load_dwordx4 v[184:187], v76, s[8:9]
	s_add_u32 s8, s8, 0x16280
	s_addc_u32 s9, s9, 0
	global_load_dwordx4 v[188:191], v76, s[8:9]
	s_add_u32 s8, s8, 0x16280
	s_addc_u32 s9, s9, 0
	global_load_dwordx4 v[192:195], v76, s[8:9]
	s_add_u32 s8, s8, 0x16280
	s_addc_u32 s9, s9, 0
	global_load_dwordx4 v[196:199], v76, s[8:9]
	s_add_u32 s8, s8, 0x16280
	s_addc_u32 s9, s9, 0
	global_load_dwordx4 v[200:203], v76, s[8:9]
	s_add_u32 s8, s8, 0x16280
	s_addc_u32 s9, s9, 0
	global_load_dwordx4 v[204:207], v76, s[8:9]
	s_add_i32 s24, s23, 64
	s_mul_i32 s20, s24, 0x80000
	s_add_u32 s6, s52, s20
	s_addc_u32 s7, s53, 0
	s_cmp_lt_u32 s24, 16
	s_cselect_b32 s20, 1, 0
	s_sub_i32 s21, s24, 16
	s_bitcmp0_b32 s21, 2
	s_cselect_b32 s21, 1, 0
	s_cmp_lt_u32 s24, 40
	s_cselect_b32 s21, s21, 0
	s_or_b32 s20, s20, s21
	s_cmp_lg_u32 s20, 0
	s_cselect_b64 s[20:21], -1, 0
	v_cndmask_b32_e64 v91, v77, v81, s[20:21]
	v_cndmask_b32_e64 v92, v78, v82, s[20:21]
	ds_read_b32 v226, v212
	ds_read_b32 v227, v212 offset:512
	ds_read_b32 v228, v212 offset:1024
	ds_read_b32 v229, v212 offset:1536
	ds_read_b32 v230, v212 offset:2048
	ds_read_b32 v231, v212 offset:2560
	ds_read_b32 v232, v212 offset:3072
	ds_read_b32 v233, v212 offset:3584
	ds_read_b32 v234, v212 offset:4096
	ds_read_b32 v235, v212 offset:4608
	ds_read_b32 v236, v212 offset:5120
	ds_read_b32 v237, v212 offset:5632
	ds_read_b32 v238, v212 offset:6144
	ds_read_b32 v239, v212 offset:6656
	ds_read_b32 v240, v212 offset:7168
	ds_read_b32 v241, v212 offset:7680
	s_waitcnt lgkmcnt(0)
	v_max_f32_e32 v226, v226, v226
	v_max_f32_e32 v227, v227, v227
	v_max_f32_e32 v228, v228, v228
	v_max_f32_e32 v229, v229, v229
	v_max_f32_e32 v230, v230, v230
	v_max_f32_e32 v231, v231, v231
	v_max_f32_e32 v232, v232, v232
	v_max_f32_e32 v233, v233, v233
	v_max_f32_e32 v234, v234, v234
	v_max_f32_e32 v235, v235, v235
	v_max_f32_e32 v236, v236, v236
	v_max_f32_e32 v237, v237, v237
	v_max_f32_e32 v238, v238, v238
	v_max_f32_e32 v239, v239, v239
	v_max_f32_e32 v240, v240, v240
	v_max_f32_e32 v241, v241, v241
	v_med3_f32 v226, v226, s62, v95
	v_med3_f32 v227, v227, s62, v95
	v_med3_f32 v228, v228, s62, v95
	v_med3_f32 v229, v229, s62, v95
	v_med3_f32 v230, v230, s62, v95
	v_med3_f32 v231, v231, s62, v95
	v_med3_f32 v232, v232, s62, v95
	v_med3_f32 v233, v233, s62, v95
	v_med3_f32 v234, v234, s62, v95
	v_med3_f32 v235, v235, s62, v95
	v_med3_f32 v236, v236, s62, v95
	v_med3_f32 v237, v237, s62, v95
	v_med3_f32 v238, v238, s62, v95
	v_med3_f32 v239, v239, s62, v95
	v_med3_f32 v240, v240, s62, v95
	v_med3_f32 v241, v241, s62, v95
	v_mov_b32_e32 v242, 0
	v_mov_b32_e32 v243, 0
	v_mov_b32_e32 v244, 0
	v_mov_b32_e32 v245, 0
	v_cvt_pk_fp8_f32 v242, v226, v227
	v_cvt_pk_fp8_f32 v243, v230, v231
	v_cvt_pk_fp8_f32 v244, v234, v235
	v_cvt_pk_fp8_f32 v245, v238, v239
	v_cvt_pk_fp8_f32 v242, v228, v229 op_sel:[0,0,1]
	v_cvt_pk_fp8_f32 v243, v232, v233 op_sel:[0,0,1]
	v_cvt_pk_fp8_f32 v244, v236, v237 op_sel:[0,0,1]
	v_cvt_pk_fp8_f32 v245, v240, v241 op_sel:[0,0,1]
	s_nop 0
	global_store_dwordx4 v91, v[242:245], s[6:7]
	ds_read_b32 v226, v214
	ds_read_b32 v227, v214 offset:512
	ds_read_b32 v228, v214 offset:1024
	ds_read_b32 v229, v214 offset:1536
	ds_read_b32 v230, v214 offset:2048
	ds_read_b32 v231, v214 offset:2560
	ds_read_b32 v232, v214 offset:3072
	ds_read_b32 v233, v214 offset:3584
	ds_read_b32 v234, v214 offset:4096
	ds_read_b32 v235, v214 offset:4608
	ds_read_b32 v236, v214 offset:5120
	ds_read_b32 v237, v214 offset:5632
	ds_read_b32 v238, v214 offset:6144
	ds_read_b32 v239, v214 offset:6656
	ds_read_b32 v240, v214 offset:7168
	ds_read_b32 v241, v214 offset:7680
	s_waitcnt lgkmcnt(0)
	v_max_f32_e32 v226, v226, v226
	v_max_f32_e32 v227, v227, v227
	v_max_f32_e32 v228, v228, v228
	v_max_f32_e32 v229, v229, v229
	v_max_f32_e32 v230, v230, v230
	v_max_f32_e32 v231, v231, v231
	v_max_f32_e32 v232, v232, v232
	v_max_f32_e32 v233, v233, v233
	v_max_f32_e32 v234, v234, v234
	v_max_f32_e32 v235, v235, v235
	v_max_f32_e32 v236, v236, v236
	v_max_f32_e32 v237, v237, v237
	v_max_f32_e32 v238, v238, v238
	v_max_f32_e32 v239, v239, v239
	v_max_f32_e32 v240, v240, v240
	v_max_f32_e32 v241, v241, v241
	v_med3_f32 v226, v226, s62, v95
	v_med3_f32 v227, v227, s62, v95
	v_med3_f32 v228, v228, s62, v95
	v_med3_f32 v229, v229, s62, v95
	v_med3_f32 v230, v230, s62, v95
	v_med3_f32 v231, v231, s62, v95
	v_med3_f32 v232, v232, s62, v95
	v_med3_f32 v233, v233, s62, v95
	v_med3_f32 v234, v234, s62, v95
	v_med3_f32 v235, v235, s62, v95
	v_med3_f32 v236, v236, s62, v95
	v_med3_f32 v237, v237, s62, v95
	v_med3_f32 v238, v238, s62, v95
	v_med3_f32 v239, v239, s62, v95
	v_med3_f32 v240, v240, s62, v95
	v_med3_f32 v241, v241, s62, v95
	v_mov_b32_e32 v242, 0
	v_mov_b32_e32 v243, 0
	v_mov_b32_e32 v244, 0
	v_mov_b32_e32 v245, 0
	v_cvt_pk_fp8_f32 v242, v226, v227
	v_cvt_pk_fp8_f32 v243, v230, v231
	v_cvt_pk_fp8_f32 v244, v234, v235
	v_cvt_pk_fp8_f32 v245, v238, v239
	v_cvt_pk_fp8_f32 v242, v228, v229 op_sel:[0,0,1]
	v_cvt_pk_fp8_f32 v243, v232, v233 op_sel:[0,0,1]
	v_cvt_pk_fp8_f32 v244, v236, v237 op_sel:[0,0,1]
	v_cvt_pk_fp8_f32 v245, v240, v241 op_sel:[0,0,1]
	s_nop 0
	global_store_dwordx4 v92, v[242:245], s[6:7]
	s_waitcnt vmcnt(12)
	v_mul_f32_e32 v144, v50, v144
	v_mul_f32_e32 v145, v50, v145
	v_mul_f32_e32 v146, v50, v146
	v_mul_f32_e32 v147, v50, v147
	ds_write_b128 v209, v[144:147]
	v_mul_f32_e32 v148, v51, v148
	v_mul_f32_e32 v149, v51, v149
	v_mul_f32_e32 v150, v51, v150
	v_mul_f32_e32 v151, v51, v151
	ds_write_b128 v209, v[148:151] offset:1024
	v_mul_f32_e32 v152, v52, v152
	v_mul_f32_e32 v153, v52, v153
	v_mul_f32_e32 v154, v52, v154
	v_mul_f32_e32 v155, v52, v155
	ds_write_b128 v209, v[152:155] offset:2048
	v_mul_f32_e32 v156, v53, v156
	v_mul_f32_e32 v157, v53, v157
	v_mul_f32_e32 v158, v53, v158
	v_mul_f32_e32 v159, v53, v159
	ds_write_b128 v209, v[156:159] offset:3072
	v_mul_f32_e32 v160, v54, v160
	v_mul_f32_e32 v161, v54, v161
	v_mul_f32_e32 v162, v54, v162
	v_mul_f32_e32 v163, v54, v163
	ds_write_b128 v209, v[160:163] offset:4096
	v_mul_f32_e32 v164, v55, v164
	v_mul_f32_e32 v165, v55, v165
	v_mul_f32_e32 v166, v55, v166
	v_mul_f32_e32 v167, v55, v167
	ds_write_b128 v209, v[164:167] offset:5120
	v_mul_f32_e32 v168, v56, v168
	v_mul_f32_e32 v169, v56, v169
	v_mul_f32_e32 v170, v56, v170
	v_mul_f32_e32 v171, v56, v171
	ds_write_b128 v209, v[168:171] offset:6144
	v_mul_f32_e32 v172, v57, v172
	v_mul_f32_e32 v173, v57, v173
	v_mul_f32_e32 v174, v57, v174
	v_mul_f32_e32 v175, v57, v175
	ds_write_b128 v209, v[172:175] offset:7168
	s_waitcnt lgkmcnt(0)
	s_barrier
; #define GAS __attribute__((address_space(1)))
; #define LAS __attribute__((address_space(3)))
; #define LDS_WAIT() asm volatile("s_waitcnt lgkmcnt(0)" ::: "memory")
; __device__ __forceinline__ unsigned pk2(float lo, float hi) { return f2bf(lo) | (f2bf(hi) << 16); }
; __device__ __forceinline__ int nat_dim(int p) { return (p >> 1) + 64 * (p & 1); }
; template <int MAP, bool KS, bool KPERM = false>
; __device__ __forceinline__ void p0_transpose_item(const float* W, int K, int Nsrc, int nblk, bf16* WT, const float* ksA, const float* ksB, int ksplit, LAS float* scr, int item, int lane) {
;     ...
;     for (int i = 0; i < 32; ++i) { const int k = k0 + 2 * i + (lane >> 5); const int ksrc = KPERM ? ((k & ~127) + nat_dim(k & 127)) : k;
;         v[i] = sc >= 0 ? W[(size_t)ksrc * Nsrc + sc] : 0.f; }
; #pragma unroll
;     for (int i = 0; i < 32; ++i) { const int kk = 2 * i + (lane >> 5); const int k = k0 + kk;
;         if (KS) v[i] *= (k < ksplit ? ksA[k] : ksB[k - ksplit]);
;         scr[kk * 33 + (lane & 31)] = v[i]; }
;     LDS_WAIT(); asm volatile("" ::: "memory");
;     const int c = lane & 7;
; #pragma unroll
;     for (int j = 0; j < 4; ++j) { const int n = (lane >> 3) + 8 * j; const LAS float* s = scr + (8 * c) * 33 + n;
;         v4u o; o.x = pk2(s[0 * 33], s[1 * 33]); o.y = pk2(s[2 * 33], s[3 * 33]); o.z = pk2(s[4 * 33], s[5 * 33]); o.w = pk2(s[6 * 33], s[7 * 33]);
;         *(GAS v4u*)(WT + (size_t)(n0 + n) * K + k0 + 8 * c) = o; }
;     ...
;     for (int i = 0; i < 32; ++i) { const int k = k0 + 2 * i + (lane >> 5); float x = v[i] * wscale; if (KS) x *= (k < ksplit ? ksA[k] : ksB[k - ksplit]); scr[(2 * i + (lane >> 5)) * 33 + (lane & 31)] = x; }
;     LDS_WAIT(); asm volatile("" ::: "memory");
;     const int c = lane & 7;
; #pragma unroll
;     for (int j = 0; j < 4; ++j) { const int n = (lane >> 3) + 8 * j; const LAS float* s = scr + (8 * c) * 33 + n;
;         const unsigned long long o = (unsigned long long)pg8::pk4_fp8(s[0 * 33], s[1 * 33], s[2 * 33], s[3 * 33]) | ((unsigned long long)pg8::pk4_fp8(s[4 * 33], s[5 * 33], s[6 * 33], s[7 * 33]) << 32);
;         *(GAS unsigned long long*)(WT + (size_t)(n0 + n) * K + k0 + 8 * c) = o; }
	s_mov_b64 s[8:9], s[54:55]
	global_load_dwordx4 v[144:147], v75, s[8:9]
	s_add_u32 s8, s8, 0x8000
	s_addc_u32 s9, s9, 0
	global_load_dwordx4 v[148:151], v75, s[8:9]
	s_add_u32 s8, s8, 0x8000
	s_addc_u32 s9, s9, 0
	global_load_dwordx4 v[152:155], v75, s[8:9]
	s_add_u32 s8, s8, 0x8000
	s_addc_u32 s9, s9, 0
	global_load_dwordx4 v[156:159], v75, s[8:9]
	s_add_u32 s8, s8, 0x8000
	s_addc_u32 s9, s9, 0
	global_load_dwordx4 v[160:163], v75, s[8:9]
	s_add_u32 s8, s8, 0x8000
	s_addc_u32 s9, s9, 0
	global_load_dwordx4 v[164:167], v75, s[8:9]
	s_add_u32 s8, s8, 0x8000
	s_addc_u32 s9, s9, 0
	global_load_dwordx4 v[168:171], v75, s[8:9]
	s_add_u32 s8, s8, 0x8000
	s_addc_u32 s9, s9, 0
	global_load_dwordx4 v[172:175], v75, s[8:9]
	s_add_i32 s24, s23, 72
	s_mul_i32 s20, s24, 0x80000
	s_add_u32 s6, s52, s20
	s_addc_u32 s7, s53, 0
	s_cmp_lt_u32 s24, 16
	s_cselect_b32 s20, 1, 0
	s_sub_i32 s21, s24, 16
	s_bitcmp0_b32 s21, 2
	s_cselect_b32 s21, 1, 0
	s_cmp_lt_u32 s24, 40
	s_cselect_b32 s21, s21, 0
	s_or_b32 s20, s20, s21
	s_cmp_lg_u32 s20, 0
	s_cselect_b64 s[20:21], -1, 0
	v_cndmask_b32_e64 v91, v77, v81, s[20:21]
	v_cndmask_b32_e64 v92, v78, v82, s[20:21]
	ds_read_b32 v226, v211
	ds_read_b32 v227, v211 offset:512
	ds_read_b32 v228, v211 offset:1024
	ds_read_b32 v229, v211 offset:1536
	ds_read_b32 v230, v211 offset:2048
	ds_read_b32 v231, v211 offset:2560
	ds_read_b32 v232, v211 offset:3072
	ds_read_b32 v233, v211 offset:3584
	ds_read_b32 v234, v211 offset:4096
	ds_read_b32 v235, v211 offset:4608
	ds_read_b32 v236, v211 offset:5120
	ds_read_b32 v237, v211 offset:5632
	ds_read_b32 v238, v211 offset:6144
	ds_read_b32 v239, v211 offset:6656
	ds_read_b32 v240, v211 offset:7168
	ds_read_b32 v241, v211 offset:7680
	s_waitcnt lgkmcnt(0)
	v_max_f32_e32 v226, v226, v226
	v_max_f32_e32 v227, v227, v227
	v_max_f32_e32 v228, v228, v228
	v_max_f32_e32 v229, v229, v229
	v_max_f32_e32 v230, v230, v230
	v_max_f32_e32 v231, v231, v231
	v_max_f32_e32 v232, v232, v232
	v_max_f32_e32 v233, v233, v233
	v_max_f32_e32 v234, v234, v234
	v_max_f32_e32 v235, v235, v235
	v_max_f32_e32 v236, v236, v236
	v_max_f32_e32 v237, v237, v237
	v_max_f32_e32 v238, v238, v238
	v_max_f32_e32 v239, v239, v239
	v_max_f32_e32 v240, v240, v240
	v_max_f32_e32 v241, v241, v241
	v_med3_f32 v226, v226, s62, v95
	v_med3_f32 v227, v227, s62, v95
	v_med3_f32 v228, v228, s62, v95
	v_med3_f32 v229, v229, s62, v95
	v_med3_f32 v230, v230, s62, v95
	v_med3_f32 v231, v231, s62, v95
	v_med3_f32 v232, v232, s62, v95
	v_med3_f32 v233, v233, s62, v95
	v_med3_f32 v234, v234, s62, v95
	v_med3_f32 v235, v235, s62, v95
	v_med3_f32 v236, v236, s62, v95
	v_med3_f32 v237, v237, s62, v95
	v_med3_f32 v238, v238, s62, v95
	v_med3_f32 v239, v239, s62, v95
	v_med3_f32 v240, v240, s62, v95
	v_med3_f32 v241, v241, s62, v95
	v_mov_b32_e32 v242, 0
	v_mov_b32_e32 v243, 0
	v_mov_b32_e32 v244, 0
	v_mov_b32_e32 v245, 0
	v_cvt_pk_fp8_f32 v242, v226, v227
	v_cvt_pk_fp8_f32 v243, v230, v231
	v_cvt_pk_fp8_f32 v244, v234, v235
	v_cvt_pk_fp8_f32 v245, v238, v239
	v_cvt_pk_fp8_f32 v242, v228, v229 op_sel:[0,0,1]
	v_cvt_pk_fp8_f32 v243, v232, v233 op_sel:[0,0,1]
	v_cvt_pk_fp8_f32 v244, v236, v237 op_sel:[0,0,1]
	v_cvt_pk_fp8_f32 v245, v240, v241 op_sel:[0,0,1]
	s_nop 0
	global_store_dwordx4 v91, v[242:245], s[6:7]
	ds_read_b32 v226, v213
	ds_read_b32 v227, v213 offset:512
	ds_read_b32 v228, v213 offset:1024
	ds_read_b32 v229, v213 offset:1536
	ds_read_b32 v230, v213 offset:2048
	ds_read_b32 v231, v213 offset:2560
	ds_read_b32 v232, v213 offset:3072
	ds_read_b32 v233, v213 offset:3584
	ds_read_b32 v234, v213 offset:4096
	ds_read_b32 v235, v213 offset:4608
	ds_read_b32 v236, v213 offset:5120
	ds_read_b32 v237, v213 offset:5632
	ds_read_b32 v238, v213 offset:6144
	ds_read_b32 v239, v213 offset:6656
	ds_read_b32 v240, v213 offset:7168
	ds_read_b32 v241, v213 offset:7680
	s_waitcnt lgkmcnt(0)
	v_max_f32_e32 v226, v226, v226
	v_max_f32_e32 v227, v227, v227
	v_max_f32_e32 v228, v228, v228
	v_max_f32_e32 v229, v229, v229
	v_max_f32_e32 v230, v230, v230
	v_max_f32_e32 v231, v231, v231
	v_max_f32_e32 v232, v232, v232
	v_max_f32_e32 v233, v233, v233
	v_max_f32_e32 v234, v234, v234
	v_max_f32_e32 v235, v235, v235
	v_max_f32_e32 v236, v236, v236
	v_max_f32_e32 v237, v237, v237
	v_max_f32_e32 v238, v238, v238
	v_max_f32_e32 v239, v239, v239
	v_max_f32_e32 v240, v240, v240
	v_max_f32_e32 v241, v241, v241
	v_med3_f32 v226, v226, s62, v95
	v_med3_f32 v227, v227, s62, v95
	v_med3_f32 v228, v228, s62, v95
	v_med3_f32 v229, v229, s62, v95
	v_med3_f32 v230, v230, s62, v95
	v_med3_f32 v231, v231, s62, v95
	v_med3_f32 v232, v232, s62, v95
	v_med3_f32 v233, v233, s62, v95
	v_med3_f32 v234, v234, s62, v95
	v_med3_f32 v235, v235, s62, v95
	v_med3_f32 v236, v236, s62, v95
	v_med3_f32 v237, v237, s62, v95
	v_med3_f32 v238, v238, s62, v95
	v_med3_f32 v239, v239, s62, v95
	v_med3_f32 v240, v240, s62, v95
	v_med3_f32 v241, v241, s62, v95
	v_mov_b32_e32 v242, 0
	v_mov_b32_e32 v243, 0
	v_mov_b32_e32 v244, 0
	v_mov_b32_e32 v245, 0
	v_cvt_pk_fp8_f32 v242, v226, v227
	v_cvt_pk_fp8_f32 v243, v230, v231
	v_cvt_pk_fp8_f32 v244, v234, v235
	v_cvt_pk_fp8_f32 v245, v238, v239
	v_cvt_pk_fp8_f32 v242, v228, v229 op_sel:[0,0,1]
	v_cvt_pk_fp8_f32 v243, v232, v233 op_sel:[0,0,1]
	v_cvt_pk_fp8_f32 v244, v236, v237 op_sel:[0,0,1]
	v_cvt_pk_fp8_f32 v245, v240, v241 op_sel:[0,0,1]
	s_nop 0
	global_store_dwordx4 v92, v[242:245], s[6:7]
	s_waitcnt vmcnt(12)
	v_mul_f32_e32 v176, v50, v176
	v_mul_f32_e32 v177, v50, v177
	v_mul_f32_e32 v178, v50, v178
	v_mul_f32_e32 v179, v50, v179
	ds_write_b128 v210, v[176:179]
	v_mul_f32_e32 v180, v51, v180
	v_mul_f32_e32 v181, v51, v181
	v_mul_f32_e32 v182, v51, v182
	v_mul_f32_e32 v183, v51, v183
	ds_write_b128 v210, v[180:183] offset:1024
	v_mul_f32_e32 v184, v52, v184
	v_mul_f32_e32 v185, v52, v185
	v_mul_f32_e32 v186, v52, v186
	v_mul_f32_e32 v187, v52, v187
	ds_write_b128 v210, v[184:187] offset:2048
	v_mul_f32_e32 v188, v53, v188
	v_mul_f32_e32 v189, v53, v189
	v_mul_f32_e32 v190, v53, v190
	v_mul_f32_e32 v191, v53, v191
	ds_write_b128 v210, v[188:191] offset:3072
	v_mul_f32_e32 v192, v54, v192
	v_mul_f32_e32 v193, v54, v193
	v_mul_f32_e32 v194, v54, v194
	v_mul_f32_e32 v195, v54, v195
	ds_write_b128 v210, v[192:195] offset:4096
	v_mul_f32_e32 v196, v55, v196
	v_mul_f32_e32 v197, v55, v197
	v_mul_f32_e32 v198, v55, v198
	v_mul_f32_e32 v199, v55, v199
	ds_write_b128 v210, v[196:199] offset:5120
	v_mul_f32_e32 v200, v56, v200
	v_mul_f32_e32 v201, v56, v201
	v_mul_f32_e32 v202, v56, v202
	v_mul_f32_e32 v203, v56, v203
	ds_write_b128 v210, v[200:203] offset:6144
	v_mul_f32_e32 v204, v57, v204
	v_mul_f32_e32 v205, v57, v205
	v_mul_f32_e32 v206, v57, v206
	v_mul_f32_e32 v207, v57, v207
	ds_write_b128 v210, v[204:207] offset:7168
	s_waitcnt lgkmcnt(0)
	s_barrier
; #define GAS __attribute__((address_space(1)))
; #define LAS __attribute__((address_space(3)))
; #define LDS_WAIT() asm volatile("s_waitcnt lgkmcnt(0)" ::: "memory")
; __device__ __forceinline__ unsigned pk2(float lo, float hi) { return f2bf(lo) | (f2bf(hi) << 16); }
; __device__ __forceinline__ int nat_dim(int p) { return (p >> 1) + 64 * (p & 1); }
; template <int MAP, bool KS, bool KPERM = false>
; __device__ __forceinline__ void p0_transpose_item(const float* W, int K, int Nsrc, int nblk, bf16* WT, const float* ksA, const float* ksB, int ksplit, LAS float* scr, int item, int lane) {
;     ...
;     for (int i = 0; i < 32; ++i) { const int k = k0 + 2 * i + (lane >> 5); const int ksrc = KPERM ? ((k & ~127) + nat_dim(k & 127)) : k;
;         v[i] = sc >= 0 ? W[(size_t)ksrc * Nsrc + sc] : 0.f; }
; #pragma unroll
;     for (int i = 0; i < 32; ++i) { const int kk = 2 * i + (lane >> 5); const int k = k0 + kk;
;         if (KS) v[i] *= (k < ksplit ? ksA[k] : ksB[k - ksplit]);
;         scr[kk * 33 + (lane & 31)] = v[i]; }
;     LDS_WAIT(); asm volatile("" ::: "memory");
;     const int c = lane & 7;
; #pragma unroll
;     for (int j = 0; j < 4; ++j) { const int n = (lane >> 3) + 8 * j; const LAS float* s = scr + (8 * c) * 33 + n;
;         v4u o; o.x = pk2(s[0 * 33], s[1 * 33]); o.y = pk2(s[2 * 33], s[3 * 33]); o.z = pk2(s[4 * 33], s[5 * 33]); o.w = pk2(s[6 * 33], s[7 * 33]);
;         *(GAS v4u*)(WT + (size_t)(n0 + n) * K + k0 + 8 * c) = o; }
;     ...
;     for (int i = 0; i < 32; ++i) { const int k = k0 + 2 * i + (lane >> 5); float x = v[i] * wscale; if (KS) x *= (k < ksplit ? ksA[k] : ksB[k - ksplit]); scr[(2 * i + (lane >> 5)) * 33 + (lane & 31)] = x; }
;     LDS_WAIT(); asm volatile("" ::: "memory");
;     const int c = lane & 7;
; #pragma unroll
;     for (int j = 0; j < 4; ++j) { const int n = (lane >> 3) + 8 * j; const LAS float* s = scr + (8 * c) * 33 + n;
;         const unsigned long long o = (unsigned long long)pg8::pk4_fp8(s[0 * 33], s[1 * 33], s[2 * 33], s[3 * 33]) | ((unsigned long long)pg8::pk4_fp8(s[4 * 33], s[5 * 33], s[6 * 33], s[7 * 33]) << 32);
;         *(GAS unsigned long long*)(WT + (size_t)(n0 + n) * K + k0 + 8 * c) = o; }
	s_add_u32 s8, s54, 0x1000
	s_addc_u32 s9, s55, 0
	global_load_dwordx4 v[176:179], v75, s[8:9]
	s_add_u32 s8, s8, 0x8000
	s_addc_u32 s9, s9, 0
	global_load_dwordx4 v[180:183], v75, s[8:9]
	s_add_u32 s8, s8, 0x8000
	s_addc_u32 s9, s9, 0
	global_load_dwordx4 v[184:187], v75, s[8:9]
	s_add_u32 s8, s8, 0x8000
	s_addc_u32 s9, s9, 0
	global_load_dwordx4 v[188:191], v75, s[8:9]
	s_add_u32 s8, s8, 0x8000
	s_addc_u32 s9, s9, 0
	global_load_dwordx4 v[192:195], v75, s[8:9]
	s_add_u32 s8, s8, 0x8000
	s_addc_u32 s9, s9, 0
	global_load_dwordx4 v[196:199], v75, s[8:9]
	s_add_u32 s8, s8, 0x8000
	s_addc_u32 s9, s9, 0
	global_load_dwordx4 v[200:203], v75, s[8:9]
	s_add_u32 s8, s8, 0x8000
	s_addc_u32 s9, s9, 0
	global_load_dwordx4 v[204:207], v75, s[8:9]
	s_add_i32 s24, s23, 80
	s_mul_i32 s20, s24, 0x80000
	s_add_u32 s6, s52, s20
	s_addc_u32 s7, s53, 0
	s_cmp_lt_u32 s24, 16
	s_cselect_b32 s20, 1, 0
	s_sub_i32 s21, s24, 16
	s_bitcmp0_b32 s21, 2
	s_cselect_b32 s21, 1, 0
	s_cmp_lt_u32 s24, 40
	s_cselect_b32 s21, s21, 0
	s_or_b32 s20, s20, s21
	s_cmp_lg_u32 s20, 0
	s_cselect_b64 s[20:21], -1, 0
	v_cndmask_b32_e64 v91, v77, v81, s[20:21]
	v_cndmask_b32_e64 v92, v78, v82, s[20:21]
	ds_read_b32 v226, v212
	ds_read_b32 v227, v212 offset:512
	ds_read_b32 v228, v212 offset:1024
	ds_read_b32 v229, v212 offset:1536
	ds_read_b32 v230, v212 offset:2048
	ds_read_b32 v231, v212 offset:2560
	ds_read_b32 v232, v212 offset:3072
	ds_read_b32 v233, v212 offset:3584
	ds_read_b32 v234, v212 offset:4096
	ds_read_b32 v235, v212 offset:4608
	ds_read_b32 v236, v212 offset:5120
	ds_read_b32 v237, v212 offset:5632
	ds_read_b32 v238, v212 offset:6144
	ds_read_b32 v239, v212 offset:6656
	ds_read_b32 v240, v212 offset:7168
	ds_read_b32 v241, v212 offset:7680
	s_waitcnt lgkmcnt(0)
	v_max_f32_e32 v226, v226, v226
	v_max_f32_e32 v227, v227, v227
	v_max_f32_e32 v228, v228, v228
	v_max_f32_e32 v229, v229, v229
	v_max_f32_e32 v230, v230, v230
	v_max_f32_e32 v231, v231, v231
	v_max_f32_e32 v232, v232, v232
	v_max_f32_e32 v233, v233, v233
	v_max_f32_e32 v234, v234, v234
	v_max_f32_e32 v235, v235, v235
	v_max_f32_e32 v236, v236, v236
	v_max_f32_e32 v237, v237, v237
	v_max_f32_e32 v238, v238, v238
	v_max_f32_e32 v239, v239, v239
	v_max_f32_e32 v240, v240, v240
	v_max_f32_e32 v241, v241, v241
	v_med3_f32 v226, v226, s62, v95
	v_med3_f32 v227, v227, s62, v95
	v_med3_f32 v228, v228, s62, v95
	v_med3_f32 v229, v229, s62, v95
	v_med3_f32 v230, v230, s62, v95
	v_med3_f32 v231, v231, s62, v95
	v_med3_f32 v232, v232, s62, v95
	v_med3_f32 v233, v233, s62, v95
	v_med3_f32 v234, v234, s62, v95
	v_med3_f32 v235, v235, s62, v95
	v_med3_f32 v236, v236, s62, v95
	v_med3_f32 v237, v237, s62, v95
	v_med3_f32 v238, v238, s62, v95
	v_med3_f32 v239, v239, s62, v95
	v_med3_f32 v240, v240, s62, v95
	v_med3_f32 v241, v241, s62, v95
	v_mov_b32_e32 v242, 0
	v_mov_b32_e32 v243, 0
	v_mov_b32_e32 v244, 0
	v_mov_b32_e32 v245, 0
	v_cvt_pk_fp8_f32 v242, v226, v227
	v_cvt_pk_fp8_f32 v243, v230, v231
	v_cvt_pk_fp8_f32 v244, v234, v235
	v_cvt_pk_fp8_f32 v245, v238, v239
	v_cvt_pk_fp8_f32 v242, v228, v229 op_sel:[0,0,1]
	v_cvt_pk_fp8_f32 v243, v232, v233 op_sel:[0,0,1]
	v_cvt_pk_fp8_f32 v244, v236, v237 op_sel:[0,0,1]
	v_cvt_pk_fp8_f32 v245, v240, v241 op_sel:[0,0,1]
	s_nop 0
	global_store_dwordx4 v91, v[242:245], s[6:7]
	ds_read_b32 v226, v214
	ds_read_b32 v227, v214 offset:512
	ds_read_b32 v228, v214 offset:1024
	ds_read_b32 v229, v214 offset:1536
	ds_read_b32 v230, v214 offset:2048
	ds_read_b32 v231, v214 offset:2560
	ds_read_b32 v232, v214 offset:3072
	ds_read_b32 v233, v214 offset:3584
	ds_read_b32 v234, v214 offset:4096
	ds_read_b32 v235, v214 offset:4608
	ds_read_b32 v236, v214 offset:5120
	ds_read_b32 v237, v214 offset:5632
	ds_read_b32 v238, v214 offset:6144
	ds_read_b32 v239, v214 offset:6656
	ds_read_b32 v240, v214 offset:7168
	ds_read_b32 v241, v214 offset:7680
	s_waitcnt lgkmcnt(0)
	v_max_f32_e32 v226, v226, v226
	v_max_f32_e32 v227, v227, v227
	v_max_f32_e32 v228, v228, v228
	v_max_f32_e32 v229, v229, v229
	v_max_f32_e32 v230, v230, v230
	v_max_f32_e32 v231, v231, v231
	v_max_f32_e32 v232, v232, v232
	v_max_f32_e32 v233, v233, v233
	v_max_f32_e32 v234, v234, v234
	v_max_f32_e32 v235, v235, v235
	v_max_f32_e32 v236, v236, v236
	v_max_f32_e32 v237, v237, v237
	v_max_f32_e32 v238, v238, v238
	v_max_f32_e32 v239, v239, v239
	v_max_f32_e32 v240, v240, v240
	v_max_f32_e32 v241, v241, v241
	v_med3_f32 v226, v226, s62, v95
	v_med3_f32 v227, v227, s62, v95
	v_med3_f32 v228, v228, s62, v95
	v_med3_f32 v229, v229, s62, v95
	v_med3_f32 v230, v230, s62, v95
	v_med3_f32 v231, v231, s62, v95
	v_med3_f32 v232, v232, s62, v95
	v_med3_f32 v233, v233, s62, v95
	v_med3_f32 v234, v234, s62, v95
	v_med3_f32 v235, v235, s62, v95
	v_med3_f32 v236, v236, s62, v95
	v_med3_f32 v237, v237, s62, v95
	v_med3_f32 v238, v238, s62, v95
	v_med3_f32 v239, v239, s62, v95
	v_med3_f32 v240, v240, s62, v95
	v_med3_f32 v241, v241, s62, v95
	v_mov_b32_e32 v242, 0
	v_mov_b32_e32 v243, 0
	v_mov_b32_e32 v244, 0
	v_mov_b32_e32 v245, 0
	v_cvt_pk_fp8_f32 v242, v226, v227
	v_cvt_pk_fp8_f32 v243, v230, v231
	v_cvt_pk_fp8_f32 v244, v234, v235
	v_cvt_pk_fp8_f32 v245, v238, v239
	v_cvt_pk_fp8_f32 v242, v228, v229 op_sel:[0,0,1]
	v_cvt_pk_fp8_f32 v243, v232, v233 op_sel:[0,0,1]
	v_cvt_pk_fp8_f32 v244, v236, v237 op_sel:[0,0,1]
	v_cvt_pk_fp8_f32 v245, v240, v241 op_sel:[0,0,1]
	s_nop 0
	global_store_dwordx4 v92, v[242:245], s[6:7]
	s_waitcnt vmcnt(12)
	v_mul_f32_e32 v144, v58, v144
	v_mul_f32_e32 v145, v58, v145
	v_mul_f32_e32 v146, v58, v146
	v_mul_f32_e32 v147, v58, v147
	ds_write_b128 v209, v[144:147]
	v_mul_f32_e32 v148, v59, v148
	v_mul_f32_e32 v149, v59, v149
	v_mul_f32_e32 v150, v59, v150
	v_mul_f32_e32 v151, v59, v151
	ds_write_b128 v209, v[148:151] offset:1024
	v_mul_f32_e32 v152, v60, v152
	v_mul_f32_e32 v153, v60, v153
	v_mul_f32_e32 v154, v60, v154
	v_mul_f32_e32 v155, v60, v155
	ds_write_b128 v209, v[152:155] offset:2048
	v_mul_f32_e32 v156, v61, v156
	v_mul_f32_e32 v157, v61, v157
	v_mul_f32_e32 v158, v61, v158
	v_mul_f32_e32 v159, v61, v159
	ds_write_b128 v209, v[156:159] offset:3072
	v_mul_f32_e32 v160, v62, v160
	v_mul_f32_e32 v161, v62, v161
	v_mul_f32_e32 v162, v62, v162
	v_mul_f32_e32 v163, v62, v163
	ds_write_b128 v209, v[160:163] offset:4096
	v_mul_f32_e32 v164, v63, v164
	v_mul_f32_e32 v165, v63, v165
	v_mul_f32_e32 v166, v63, v166
	v_mul_f32_e32 v167, v63, v167
	ds_write_b128 v209, v[164:167] offset:5120
	v_mul_f32_e32 v168, v64, v168
	v_mul_f32_e32 v169, v64, v169
	v_mul_f32_e32 v170, v64, v170
	v_mul_f32_e32 v171, v64, v171
	ds_write_b128 v209, v[168:171] offset:6144
	v_mul_f32_e32 v172, v65, v172
	v_mul_f32_e32 v173, v65, v173
	v_mul_f32_e32 v174, v65, v174
	v_mul_f32_e32 v175, v65, v175
	ds_write_b128 v209, v[172:175] offset:7168
	s_waitcnt lgkmcnt(0)
	s_barrier
; #define GAS __attribute__((address_space(1)))
; #define LAS __attribute__((address_space(3)))
; #define LDS_WAIT() asm volatile("s_waitcnt lgkmcnt(0)" ::: "memory")
; __device__ __forceinline__ unsigned f2bf(float f) { unsigned u = __builtin_bit_cast(unsigned, f); return (u + 0x7fffu + ((u >> 16) & 1u)) >> 16; }
; __device__ __forceinline__ unsigned pk2(float lo, float hi) { return f2bf(lo) | (f2bf(hi) << 16); }
; template <int MAP, bool KS, bool KPERM = false>
; __device__ __forceinline__ void p0_transpose_item(const float* W, int K, int Nsrc, int nblk, bf16* WT, const float* ksA, const float* ksB, int ksplit, LAS float* scr, int item, int lane) {
;     ...
;     for (int i = 0; i < 32; ++i) { const int kk = 2 * i + (lane >> 5); const int k = k0 + kk;
;         if (KS) v[i] *= (k < ksplit ? ksA[k] : ksB[k - ksplit]);
;         scr[kk * 33 + (lane & 31)] = v[i]; }
;     LDS_WAIT(); asm volatile("" ::: "memory");
;     const int c = lane & 7;
; #pragma unroll
;     for (int j = 0; j < 4; ++j) { const int n = (lane >> 3) + 8 * j; const LAS float* s = scr + (8 * c) * 33 + n;
;         v4u o; o.x = pk2(s[0 * 33], s[1 * 33]); o.y = pk2(s[2 * 33], s[3 * 33]); o.z = pk2(s[4 * 33], s[5 * 33]); o.w = pk2(s[6 * 33], s[7 * 33]);
;         *(GAS v4u*)(WT + (size_t)(n0 + n) * K + k0 + 8 * c) = o; }
;     LDS_WAIT(); asm volatile("" ::: "memory");
	s_add_u32 s8, s54, 0x2000
	s_addc_u32 s9, s55, 0
	global_load_dwordx4 v[144:147], v75, s[8:9]
	s_add_u32 s8, s8, 0x8000
	s_addc_u32 s9, s9, 0
	global_load_dwordx4 v[148:151], v75, s[8:9]
	s_add_u32 s8, s8, 0x8000
	s_addc_u32 s9, s9, 0
	global_load_dwordx4 v[152:155], v75, s[8:9]
	s_add_u32 s8, s8, 0x8000
	s_addc_u32 s9, s9, 0
	global_load_dwordx4 v[156:159], v75, s[8:9]
	s_add_u32 s8, s8, 0x8000
	s_addc_u32 s9, s9, 0
	global_load_dwordx4 v[160:163], v75, s[8:9]
	s_add_u32 s8, s8, 0x8000
	s_addc_u32 s9, s9, 0
	global_load_dwordx4 v[164:167], v75, s[8:9]
	s_add_u32 s8, s8, 0x8000
	s_addc_u32 s9, s9, 0
	global_load_dwordx4 v[168:171], v75, s[8:9]
	s_add_u32 s8, s8, 0x8000
	s_addc_u32 s9, s9, 0
	global_load_dwordx4 v[172:175], v75, s[8:9]
	s_mov_b64 s[6:7], s[56:57]
	ds_read_b32 v226, v112
	ds_read_b32 v227, v112 offset:512
	ds_read_b32 v228, v112 offset:1024
	ds_read_b32 v229, v112 offset:1536
	ds_read_b32 v230, v112 offset:2048
	ds_read_b32 v231, v112 offset:2560
	ds_read_b32 v232, v112 offset:3072
	ds_read_b32 v233, v112 offset:3584
	s_waitcnt lgkmcnt(0)
	v_bfe_u32 v120, v226, 16, 1
	v_bfe_u32 v121, v227, 16, 1
	v_bfe_u32 v122, v228, 16, 1
	v_bfe_u32 v123, v229, 16, 1
	v_bfe_u32 v124, v230, 16, 1
	v_bfe_u32 v125, v231, 16, 1
	v_bfe_u32 v126, v232, 16, 1
	v_bfe_u32 v127, v233, 16, 1
	v_add3_u32 v226, v226, v120, s63
	v_add3_u32 v227, v227, v121, s63
	v_add3_u32 v228, v228, v122, s63
	v_add3_u32 v229, v229, v123, s63
	v_add3_u32 v230, v230, v124, s63
	v_add3_u32 v231, v231, v125, s63
	v_add3_u32 v232, v232, v126, s63
	v_add3_u32 v233, v233, v127, s63
	v_perm_b32 v242, v227, v226, s64
	v_perm_b32 v243, v229, v228, s64
	v_perm_b32 v244, v231, v230, s64
	v_perm_b32 v245, v233, v232, s64
	s_nop 0
	global_store_dwordx4 v83, v[242:245], s[6:7]
	ds_read_b32 v226, v114
	ds_read_b32 v227, v114 offset:512
	ds_read_b32 v228, v114 offset:1024
	ds_read_b32 v229, v114 offset:1536
	ds_read_b32 v230, v114 offset:2048
	ds_read_b32 v231, v114 offset:2560
	ds_read_b32 v232, v114 offset:3072
	ds_read_b32 v233, v114 offset:3584
	s_waitcnt lgkmcnt(0)
	v_bfe_u32 v120, v226, 16, 1
	v_bfe_u32 v121, v227, 16, 1
	v_bfe_u32 v122, v228, 16, 1
	v_bfe_u32 v123, v229, 16, 1
	v_bfe_u32 v124, v230, 16, 1
	v_bfe_u32 v125, v231, 16, 1
	v_bfe_u32 v126, v232, 16, 1
	v_bfe_u32 v127, v233, 16, 1
	v_add3_u32 v226, v226, v120, s63
	v_add3_u32 v227, v227, v121, s63
	v_add3_u32 v228, v228, v122, s63
	v_add3_u32 v229, v229, v123, s63
	v_add3_u32 v230, v230, v124, s63
	v_add3_u32 v231, v231, v125, s63
	v_add3_u32 v232, v232, v126, s63
	v_add3_u32 v233, v233, v127, s63
	v_perm_b32 v242, v227, v226, s64
	v_perm_b32 v243, v229, v228, s64
	v_perm_b32 v244, v231, v230, s64
	v_perm_b32 v245, v233, v232, s64
	s_nop 0
	global_store_dwordx4 v84, v[242:245], s[6:7]
	ds_read_b32 v226, v116
	ds_read_b32 v227, v116 offset:512
	ds_read_b32 v228, v116 offset:1024
	ds_read_b32 v229, v116 offset:1536
	ds_read_b32 v230, v116 offset:2048
	ds_read_b32 v231, v116 offset:2560
	ds_read_b32 v232, v116 offset:3072
	ds_read_b32 v233, v116 offset:3584
	s_waitcnt lgkmcnt(0)
	v_bfe_u32 v120, v226, 16, 1
	v_bfe_u32 v121, v227, 16, 1
	v_bfe_u32 v122, v228, 16, 1
	v_bfe_u32 v123, v229, 16, 1
	v_bfe_u32 v124, v230, 16, 1
	v_bfe_u32 v125, v231, 16, 1
	v_bfe_u32 v126, v232, 16, 1
	v_bfe_u32 v127, v233, 16, 1
	v_add3_u32 v226, v226, v120, s63
	v_add3_u32 v227, v227, v121, s63
	v_add3_u32 v228, v228, v122, s63
	v_add3_u32 v229, v229, v123, s63
	v_add3_u32 v230, v230, v124, s63
	v_add3_u32 v231, v231, v125, s63
	v_add3_u32 v232, v232, v126, s63
	v_add3_u32 v233, v233, v127, s63
	v_perm_b32 v242, v227, v226, s64
	v_perm_b32 v243, v229, v228, s64
	v_perm_b32 v244, v231, v230, s64
	v_perm_b32 v245, v233, v232, s64
	s_nop 0
	global_store_dwordx4 v85, v[242:245], s[6:7]
	ds_read_b32 v226, v118
	ds_read_b32 v227, v118 offset:512
	ds_read_b32 v228, v118 offset:1024
	ds_read_b32 v229, v118 offset:1536
	ds_read_b32 v230, v118 offset:2048
	ds_read_b32 v231, v118 offset:2560
	ds_read_b32 v232, v118 offset:3072
	ds_read_b32 v233, v118 offset:3584
	s_waitcnt lgkmcnt(0)
	v_bfe_u32 v120, v226, 16, 1
	v_bfe_u32 v121, v227, 16, 1
	v_bfe_u32 v122, v228, 16, 1
	v_bfe_u32 v123, v229, 16, 1
	v_bfe_u32 v124, v230, 16, 1
	v_bfe_u32 v125, v231, 16, 1
	v_bfe_u32 v126, v232, 16, 1
	v_bfe_u32 v127, v233, 16, 1
	v_add3_u32 v226, v226, v120, s63
	v_add3_u32 v227, v227, v121, s63
	v_add3_u32 v228, v228, v122, s63
	v_add3_u32 v229, v229, v123, s63
	v_add3_u32 v230, v230, v124, s63
	v_add3_u32 v231, v231, v125, s63
	v_add3_u32 v232, v232, v126, s63
	v_add3_u32 v233, v233, v127, s63
	v_perm_b32 v242, v227, v226, s64
	v_perm_b32 v243, v229, v228, s64
	v_perm_b32 v244, v231, v230, s64
	v_perm_b32 v245, v233, v232, s64
	s_nop 0
	global_store_dwordx4 v86, v[242:245], s[6:7]
	s_waitcnt vmcnt(14)
	v_mul_f32_e32 v176, v58, v176
	v_mul_f32_e32 v177, v58, v177
	v_mul_f32_e32 v178, v58, v178
	v_mul_f32_e32 v179, v58, v179
	ds_write_b128 v210, v[176:179]
	v_mul_f32_e32 v180, v59, v180
	v_mul_f32_e32 v181, v59, v181
	v_mul_f32_e32 v182, v59, v182
	v_mul_f32_e32 v183, v59, v183
	ds_write_b128 v210, v[180:183] offset:1024
	v_mul_f32_e32 v184, v60, v184
	v_mul_f32_e32 v185, v60, v185
	v_mul_f32_e32 v186, v60, v186
	v_mul_f32_e32 v187, v60, v187
	ds_write_b128 v210, v[184:187] offset:2048
	v_mul_f32_e32 v188, v61, v188
	v_mul_f32_e32 v189, v61, v189
	v_mul_f32_e32 v190, v61, v190
	v_mul_f32_e32 v191, v61, v191
	ds_write_b128 v210, v[188:191] offset:3072
	v_mul_f32_e32 v192, v62, v192
	v_mul_f32_e32 v193, v62, v193
	v_mul_f32_e32 v194, v62, v194
	v_mul_f32_e32 v195, v62, v195
	ds_write_b128 v210, v[192:195] offset:4096
	v_mul_f32_e32 v196, v63, v196
	v_mul_f32_e32 v197, v63, v197
	v_mul_f32_e32 v198, v63, v198
	v_mul_f32_e32 v199, v63, v199
	ds_write_b128 v210, v[196:199] offset:5120
	v_mul_f32_e32 v200, v64, v200
	v_mul_f32_e32 v201, v64, v201
	v_mul_f32_e32 v202, v64, v202
	v_mul_f32_e32 v203, v64, v203
	ds_write_b128 v210, v[200:203] offset:6144
	v_mul_f32_e32 v204, v65, v204
	v_mul_f32_e32 v205, v65, v205
	v_mul_f32_e32 v206, v65, v206
	v_mul_f32_e32 v207, v65, v207
	ds_write_b128 v210, v[204:207] offset:7168
	s_waitcnt lgkmcnt(0)
	s_barrier
; #define GAS __attribute__((address_space(1)))
; #define LAS __attribute__((address_space(3)))
; #define LDS_WAIT() asm volatile("s_waitcnt lgkmcnt(0)" ::: "memory")
; __device__ __forceinline__ unsigned f2bf(float f) { unsigned u = __builtin_bit_cast(unsigned, f); return (u + 0x7fffu + ((u >> 16) & 1u)) >> 16; }
; __device__ __forceinline__ unsigned pk2(float lo, float hi) { return f2bf(lo) | (f2bf(hi) << 16); }
; template <int MAP, bool KS, bool KPERM = false>
; __device__ __forceinline__ void p0_transpose_item(const float* W, int K, int Nsrc, int nblk, bf16* WT, const float* ksA, const float* ksB, int ksplit, LAS float* scr, int item, int lane) {
;     ...
;     for (int i = 0; i < 32; ++i) { const int kk = 2 * i + (lane >> 5); const int k = k0 + kk;
;         if (KS) v[i] *= (k < ksplit ? ksA[k] : ksB[k - ksplit]);
;         scr[kk * 33 + (lane & 31)] = v[i]; }
;     LDS_WAIT(); asm volatile("" ::: "memory");
;     const int c = lane & 7;
; #pragma unroll
;     for (int j = 0; j < 4; ++j) { const int n = (lane >> 3) + 8 * j; const LAS float* s = scr + (8 * c) * 33 + n;
;         v4u o; o.x = pk2(s[0 * 33], s[1 * 33]); o.y = pk2(s[2 * 33], s[3 * 33]); o.z = pk2(s[4 * 33], s[5 * 33]); o.w = pk2(s[6 * 33], s[7 * 33]);
;         *(GAS v4u*)(WT + (size_t)(n0 + n) * K + k0 + 8 * c) = o; }
;     LDS_WAIT(); asm volatile("" ::: "memory");
	s_add_u32 s8, s54, 0x3000
	s_addc_u32 s9, s55, 0
	global_load_dwordx4 v[176:179], v75, s[8:9]
	s_add_u32 s8, s8, 0x8000
	s_addc_u32 s9, s9, 0
	global_load_dwordx4 v[180:183], v75, s[8:9]
	s_add_u32 s8, s8, 0x8000
	s_addc_u32 s9, s9, 0
	global_load_dwordx4 v[184:187], v75, s[8:9]
	s_add_u32 s8, s8, 0x8000
	s_addc_u32 s9, s9, 0
	global_load_dwordx4 v[188:191], v75, s[8:9]
	s_add_u32 s8, s8, 0x8000
	s_addc_u32 s9, s9, 0
	global_load_dwordx4 v[192:195], v75, s[8:9]
	s_add_u32 s8, s8, 0x8000
	s_addc_u32 s9, s9, 0
	global_load_dwordx4 v[196:199], v75, s[8:9]
	s_add_u32 s8, s8, 0x8000
	s_addc_u32 s9, s9, 0
	global_load_dwordx4 v[200:203], v75, s[8:9]
	s_add_u32 s8, s8, 0x8000
	s_addc_u32 s9, s9, 0
	global_load_dwordx4 v[204:207], v75, s[8:9]
	s_add_u32 s6, s56, 0x800000
	s_addc_u32 s7, s57, 0
	ds_read_b32 v226, v113
	ds_read_b32 v227, v113 offset:512
	ds_read_b32 v228, v113 offset:1024
	ds_read_b32 v229, v113 offset:1536
	ds_read_b32 v230, v113 offset:2048
	ds_read_b32 v231, v113 offset:2560
	ds_read_b32 v232, v113 offset:3072
	ds_read_b32 v233, v113 offset:3584
	s_waitcnt lgkmcnt(0)
	v_bfe_u32 v120, v226, 16, 1
	v_bfe_u32 v121, v227, 16, 1
	v_bfe_u32 v122, v228, 16, 1
	v_bfe_u32 v123, v229, 16, 1
	v_bfe_u32 v124, v230, 16, 1
	v_bfe_u32 v125, v231, 16, 1
	v_bfe_u32 v126, v232, 16, 1
	v_bfe_u32 v127, v233, 16, 1
	v_add3_u32 v226, v226, v120, s63
	v_add3_u32 v227, v227, v121, s63
	v_add3_u32 v228, v228, v122, s63
	v_add3_u32 v229, v229, v123, s63
	v_add3_u32 v230, v230, v124, s63
	v_add3_u32 v231, v231, v125, s63
	v_add3_u32 v232, v232, v126, s63
	v_add3_u32 v233, v233, v127, s63
	v_perm_b32 v242, v227, v226, s64
	v_perm_b32 v243, v229, v228, s64
	v_perm_b32 v244, v231, v230, s64
	v_perm_b32 v245, v233, v232, s64
	s_nop 0
	global_store_dwordx4 v83, v[242:245], s[6:7]
	ds_read_b32 v226, v115
	ds_read_b32 v227, v115 offset:512
	ds_read_b32 v228, v115 offset:1024
	ds_read_b32 v229, v115 offset:1536
	ds_read_b32 v230, v115 offset:2048
	ds_read_b32 v231, v115 offset:2560
	ds_read_b32 v232, v115 offset:3072
	ds_read_b32 v233, v115 offset:3584
	s_waitcnt lgkmcnt(0)
	v_bfe_u32 v120, v226, 16, 1
	v_bfe_u32 v121, v227, 16, 1
	v_bfe_u32 v122, v228, 16, 1
	v_bfe_u32 v123, v229, 16, 1
	v_bfe_u32 v124, v230, 16, 1
	v_bfe_u32 v125, v231, 16, 1
	v_bfe_u32 v126, v232, 16, 1
	v_bfe_u32 v127, v233, 16, 1
	v_add3_u32 v226, v226, v120, s63
	v_add3_u32 v227, v227, v121, s63
	v_add3_u32 v228, v228, v122, s63
	v_add3_u32 v229, v229, v123, s63
	v_add3_u32 v230, v230, v124, s63
	v_add3_u32 v231, v231, v125, s63
	v_add3_u32 v232, v232, v126, s63
	v_add3_u32 v233, v233, v127, s63
	v_perm_b32 v242, v227, v226, s64
	v_perm_b32 v243, v229, v228, s64
	v_perm_b32 v244, v231, v230, s64
	v_perm_b32 v245, v233, v232, s64
	s_nop 0
	global_store_dwordx4 v84, v[242:245], s[6:7]
	ds_read_b32 v226, v117
	ds_read_b32 v227, v117 offset:512
	ds_read_b32 v228, v117 offset:1024
	ds_read_b32 v229, v117 offset:1536
	ds_read_b32 v230, v117 offset:2048
	ds_read_b32 v231, v117 offset:2560
	ds_read_b32 v232, v117 offset:3072
	ds_read_b32 v233, v117 offset:3584
	s_waitcnt lgkmcnt(0)
	v_bfe_u32 v120, v226, 16, 1
	v_bfe_u32 v121, v227, 16, 1
	v_bfe_u32 v122, v228, 16, 1
	v_bfe_u32 v123, v229, 16, 1
	v_bfe_u32 v124, v230, 16, 1
	v_bfe_u32 v125, v231, 16, 1
	v_bfe_u32 v126, v232, 16, 1
	v_bfe_u32 v127, v233, 16, 1
	v_add3_u32 v226, v226, v120, s63
	v_add3_u32 v227, v227, v121, s63
	v_add3_u32 v228, v228, v122, s63
	v_add3_u32 v229, v229, v123, s63
	v_add3_u32 v230, v230, v124, s63
	v_add3_u32 v231, v231, v125, s63
	v_add3_u32 v232, v232, v126, s63
	v_add3_u32 v233, v233, v127, s63
	v_perm_b32 v242, v227, v226, s64
	v_perm_b32 v243, v229, v228, s64
	v_perm_b32 v244, v231, v230, s64
	v_perm_b32 v245, v233, v232, s64
	s_nop 0
	global_store_dwordx4 v85, v[242:245], s[6:7]
	ds_read_b32 v226, v119
	ds_read_b32 v227, v119 offset:512
	ds_read_b32 v228, v119 offset:1024
	ds_read_b32 v229, v119 offset:1536
	ds_read_b32 v230, v119 offset:2048
	ds_read_b32 v231, v119 offset:2560
	ds_read_b32 v232, v119 offset:3072
	ds_read_b32 v233, v119 offset:3584
	s_waitcnt lgkmcnt(0)
	v_bfe_u32 v120, v226, 16, 1
	v_bfe_u32 v121, v227, 16, 1
	v_bfe_u32 v122, v228, 16, 1
	v_bfe_u32 v123, v229, 16, 1
	v_bfe_u32 v124, v230, 16, 1
	v_bfe_u32 v125, v231, 16, 1
	v_bfe_u32 v126, v232, 16, 1
	v_bfe_u32 v127, v233, 16, 1
	v_add3_u32 v226, v226, v120, s63
	v_add3_u32 v227, v227, v121, s63
	v_add3_u32 v228, v228, v122, s63
	v_add3_u32 v229, v229, v123, s63
	v_add3_u32 v230, v230, v124, s63
	v_add3_u32 v231, v231, v125, s63
	v_add3_u32 v232, v232, v126, s63
	v_add3_u32 v233, v233, v127, s63
	v_perm_b32 v242, v227, v226, s64
	v_perm_b32 v243, v229, v228, s64
	v_perm_b32 v244, v231, v230, s64
	v_perm_b32 v245, v233, v232, s64
	s_nop 0
	global_store_dwordx4 v86, v[242:245], s[6:7]
	s_waitcnt vmcnt(16)
	v_mul_f32_e32 v144, v58, v144
	v_mul_f32_e32 v145, v58, v145
	v_mul_f32_e32 v146, v58, v146
	v_mul_f32_e32 v147, v58, v147
	ds_write_b128 v209, v[144:147]
	v_mul_f32_e32 v148, v59, v148
	v_mul_f32_e32 v149, v59, v149
	v_mul_f32_e32 v150, v59, v150
	v_mul_f32_e32 v151, v59, v151
	ds_write_b128 v209, v[148:151] offset:1024
	v_mul_f32_e32 v152, v60, v152
	v_mul_f32_e32 v153, v60, v153
	v_mul_f32_e32 v154, v60, v154
	v_mul_f32_e32 v155, v60, v155
	ds_write_b128 v209, v[152:155] offset:2048
	v_mul_f32_e32 v156, v61, v156
	v_mul_f32_e32 v157, v61, v157
	v_mul_f32_e32 v158, v61, v158
	v_mul_f32_e32 v159, v61, v159
	ds_write_b128 v209, v[156:159] offset:3072
	v_mul_f32_e32 v160, v62, v160
	v_mul_f32_e32 v161, v62, v161
	v_mul_f32_e32 v162, v62, v162
	v_mul_f32_e32 v163, v62, v163
	ds_write_b128 v209, v[160:163] offset:4096
	v_mul_f32_e32 v164, v63, v164
	v_mul_f32_e32 v165, v63, v165
	v_mul_f32_e32 v166, v63, v166
	v_mul_f32_e32 v167, v63, v167
	ds_write_b128 v209, v[164:167] offset:5120
	v_mul_f32_e32 v168, v64, v168
	v_mul_f32_e32 v169, v64, v169
	v_mul_f32_e32 v170, v64, v170
	v_mul_f32_e32 v171, v64, v171
	ds_write_b128 v209, v[168:171] offset:6144
	v_mul_f32_e32 v172, v65, v172
	v_mul_f32_e32 v173, v65, v173
	v_mul_f32_e32 v174, v65, v174
	v_mul_f32_e32 v175, v65, v175
	ds_write_b128 v209, v[172:175] offset:7168
	s_waitcnt lgkmcnt(0)
	s_barrier
; #define GAS __attribute__((address_space(1)))
; #define LAS __attribute__((address_space(3)))
; #define LDS_WAIT() asm volatile("s_waitcnt lgkmcnt(0)" ::: "memory")
; __device__ __forceinline__ unsigned f2bf(float f) { unsigned u = __builtin_bit_cast(unsigned, f); return (u + 0x7fffu + ((u >> 16) & 1u)) >> 16; }
; __device__ __forceinline__ unsigned pk2(float lo, float hi) { return f2bf(lo) | (f2bf(hi) << 16); }
; template <int MAP, bool KS, bool KPERM = false>
; __device__ __forceinline__ void p0_transpose_item(const float* W, int K, int Nsrc, int nblk, bf16* WT, const float* ksA, const float* ksB, int ksplit, LAS float* scr, int item, int lane) {
;     ...
;     for (int i = 0; i < 32; ++i) { const int kk = 2 * i + (lane >> 5); const int k = k0 + kk;
;         if (KS) v[i] *= (k < ksplit ? ksA[k] : ksB[k - ksplit]);
;         scr[kk * 33 + (lane & 31)] = v[i]; }
;     LDS_WAIT(); asm volatile("" ::: "memory");
;     const int c = lane & 7;
; #pragma unroll
;     for (int j = 0; j < 4; ++j) { const int n = (lane >> 3) + 8 * j; const LAS float* s = scr + (8 * c) * 33 + n;
;         v4u o; o.x = pk2(s[0 * 33], s[1 * 33]); o.y = pk2(s[2 * 33], s[3 * 33]); o.z = pk2(s[4 * 33], s[5 * 33]); o.w = pk2(s[6 * 33], s[7 * 33]);
;         *(GAS v4u*)(WT + (size_t)(n0 + n) * K + k0 + 8 * c) = o; }
;     LDS_WAIT(); asm volatile("" ::: "memory");
	s_add_u32 s6, s56, 0x1000000
	s_addc_u32 s7, s57, 0
	ds_read_b32 v226, v112
	ds_read_b32 v227, v112 offset:512
	ds_read_b32 v228, v112 offset:1024
	ds_read_b32 v229, v112 offset:1536
	ds_read_b32 v230, v112 offset:2048
	ds_read_b32 v231, v112 offset:2560
	ds_read_b32 v232, v112 offset:3072
	ds_read_b32 v233, v112 offset:3584
	s_waitcnt lgkmcnt(0)
	v_bfe_u32 v120, v226, 16, 1
	v_bfe_u32 v121, v227, 16, 1
	v_bfe_u32 v122, v228, 16, 1
	v_bfe_u32 v123, v229, 16, 1
	v_bfe_u32 v124, v230, 16, 1
	v_bfe_u32 v125, v231, 16, 1
	v_bfe_u32 v126, v232, 16, 1
	v_bfe_u32 v127, v233, 16, 1
	v_add3_u32 v226, v226, v120, s63
	v_add3_u32 v227, v227, v121, s63
	v_add3_u32 v228, v228, v122, s63
	v_add3_u32 v229, v229, v123, s63
	v_add3_u32 v230, v230, v124, s63
	v_add3_u32 v231, v231, v125, s63
	v_add3_u32 v232, v232, v126, s63
	v_add3_u32 v233, v233, v127, s63
	v_perm_b32 v242, v227, v226, s64
	v_perm_b32 v243, v229, v228, s64
	v_perm_b32 v244, v231, v230, s64
	v_perm_b32 v245, v233, v232, s64
	s_nop 0
	global_store_dwordx4 v83, v[242:245], s[6:7]
	ds_read_b32 v226, v114
	ds_read_b32 v227, v114 offset:512
	ds_read_b32 v228, v114 offset:1024
	ds_read_b32 v229, v114 offset:1536
	ds_read_b32 v230, v114 offset:2048
	ds_read_b32 v231, v114 offset:2560
	ds_read_b32 v232, v114 offset:3072
	ds_read_b32 v233, v114 offset:3584
	s_waitcnt lgkmcnt(0)
	v_bfe_u32 v120, v226, 16, 1
	v_bfe_u32 v121, v227, 16, 1
	v_bfe_u32 v122, v228, 16, 1
	v_bfe_u32 v123, v229, 16, 1
	v_bfe_u32 v124, v230, 16, 1
	v_bfe_u32 v125, v231, 16, 1
	v_bfe_u32 v126, v232, 16, 1
	v_bfe_u32 v127, v233, 16, 1
	v_add3_u32 v226, v226, v120, s63
	v_add3_u32 v227, v227, v121, s63
	v_add3_u32 v228, v228, v122, s63
	v_add3_u32 v229, v229, v123, s63
	v_add3_u32 v230, v230, v124, s63
	v_add3_u32 v231, v231, v125, s63
	v_add3_u32 v232, v232, v126, s63
	v_add3_u32 v233, v233, v127, s63
	v_perm_b32 v242, v227, v226, s64
	v_perm_b32 v243, v229, v228, s64
	v_perm_b32 v244, v231, v230, s64
	v_perm_b32 v245, v233, v232, s64
	s_nop 0
	global_store_dwordx4 v84, v[242:245], s[6:7]
	ds_read_b32 v226, v116
	ds_read_b32 v227, v116 offset:512
	ds_read_b32 v228, v116 offset:1024
	ds_read_b32 v229, v116 offset:1536
	ds_read_b32 v230, v116 offset:2048
	ds_read_b32 v231, v116 offset:2560
	ds_read_b32 v232, v116 offset:3072
	ds_read_b32 v233, v116 offset:3584
	s_waitcnt lgkmcnt(0)
	v_bfe_u32 v120, v226, 16, 1
	v_bfe_u32 v121, v227, 16, 1
	v_bfe_u32 v122, v228, 16, 1
	v_bfe_u32 v123, v229, 16, 1
	v_bfe_u32 v124, v230, 16, 1
	v_bfe_u32 v125, v231, 16, 1
	v_bfe_u32 v126, v232, 16, 1
	v_bfe_u32 v127, v233, 16, 1
	v_add3_u32 v226, v226, v120, s63
	v_add3_u32 v227, v227, v121, s63
	v_add3_u32 v228, v228, v122, s63
	v_add3_u32 v229, v229, v123, s63
	v_add3_u32 v230, v230, v124, s63
	v_add3_u32 v231, v231, v125, s63
	v_add3_u32 v232, v232, v126, s63
	v_add3_u32 v233, v233, v127, s63
	v_perm_b32 v242, v227, v226, s64
	v_perm_b32 v243, v229, v228, s64
	v_perm_b32 v244, v231, v230, s64
	v_perm_b32 v245, v233, v232, s64
	s_nop 0
	global_store_dwordx4 v85, v[242:245], s[6:7]
	ds_read_b32 v226, v118
	ds_read_b32 v227, v118 offset:512
	ds_read_b32 v228, v118 offset:1024
	ds_read_b32 v229, v118 offset:1536
	ds_read_b32 v230, v118 offset:2048
	ds_read_b32 v231, v118 offset:2560
	ds_read_b32 v232, v118 offset:3072
	ds_read_b32 v233, v118 offset:3584
	s_waitcnt lgkmcnt(0)
	v_bfe_u32 v120, v226, 16, 1
	v_bfe_u32 v121, v227, 16, 1
	v_bfe_u32 v122, v228, 16, 1
	v_bfe_u32 v123, v229, 16, 1
	v_bfe_u32 v124, v230, 16, 1
	v_bfe_u32 v125, v231, 16, 1
	v_bfe_u32 v126, v232, 16, 1
	v_bfe_u32 v127, v233, 16, 1
	v_add3_u32 v226, v226, v120, s63
	v_add3_u32 v227, v227, v121, s63
	v_add3_u32 v228, v228, v122, s63
	v_add3_u32 v229, v229, v123, s63
	v_add3_u32 v230, v230, v124, s63
	v_add3_u32 v231, v231, v125, s63
	v_add3_u32 v232, v232, v126, s63
	v_add3_u32 v233, v233, v127, s63
	v_perm_b32 v242, v227, v226, s64
	v_perm_b32 v243, v229, v228, s64
	v_perm_b32 v244, v231, v230, s64
	v_perm_b32 v245, v233, v232, s64
	s_nop 0
	global_store_dwordx4 v86, v[242:245], s[6:7]
	s_waitcnt vmcnt(8)
	v_mul_f32_e32 v176, v58, v176
	v_mul_f32_e32 v177, v58, v177
	v_mul_f32_e32 v178, v58, v178
	v_mul_f32_e32 v179, v58, v179
	ds_write_b128 v210, v[176:179]
	v_mul_f32_e32 v180, v59, v180
	v_mul_f32_e32 v181, v59, v181
	v_mul_f32_e32 v182, v59, v182
	v_mul_f32_e32 v183, v59, v183
	ds_write_b128 v210, v[180:183] offset:1024
	v_mul_f32_e32 v184, v60, v184
	v_mul_f32_e32 v185, v60, v185
	v_mul_f32_e32 v186, v60, v186
	v_mul_f32_e32 v187, v60, v187
	ds_write_b128 v210, v[184:187] offset:2048
	v_mul_f32_e32 v188, v61, v188
	v_mul_f32_e32 v189, v61, v189
	v_mul_f32_e32 v190, v61, v190
	v_mul_f32_e32 v191, v61, v191
	ds_write_b128 v210, v[188:191] offset:3072
	v_mul_f32_e32 v192, v62, v192
	v_mul_f32_e32 v193, v62, v193
	v_mul_f32_e32 v194, v62, v194
	v_mul_f32_e32 v195, v62, v195
	ds_write_b128 v210, v[192:195] offset:4096
	v_mul_f32_e32 v196, v63, v196
	v_mul_f32_e32 v197, v63, v197
	v_mul_f32_e32 v198, v63, v198
	v_mul_f32_e32 v199, v63, v199
	ds_write_b128 v210, v[196:199] offset:5120
	v_mul_f32_e32 v200, v64, v200
	v_mul_f32_e32 v201, v64, v201
	v_mul_f32_e32 v202, v64, v202
	v_mul_f32_e32 v203, v64, v203
	ds_write_b128 v210, v[200:203] offset:6144
	v_mul_f32_e32 v204, v65, v204
	v_mul_f32_e32 v205, v65, v205
	v_mul_f32_e32 v206, v65, v206
	v_mul_f32_e32 v207, v65, v207
	ds_write_b128 v210, v[204:207] offset:7168
	s_waitcnt lgkmcnt(0)
	s_barrier
; #define GAS __attribute__((address_space(1)))
; #define LAS __attribute__((address_space(3)))
; #define LDS_WAIT() asm volatile("s_waitcnt lgkmcnt(0)" ::: "memory")
; __device__ __forceinline__ unsigned f2bf(float f) { unsigned u = __builtin_bit_cast(unsigned, f); return (u + 0x7fffu + ((u >> 16) & 1u)) >> 16; }
; __device__ __forceinline__ unsigned pk2(float lo, float hi) { return f2bf(lo) | (f2bf(hi) << 16); }
; template <int MAP, bool KS, bool KPERM = false>
; __device__ __forceinline__ void p0_transpose_item(const float* W, int K, int Nsrc, int nblk, bf16* WT, const float* ksA, const float* ksB, int ksplit, LAS float* scr, int item, int lane) {
;     ...
;     for (int i = 0; i < 32; ++i) { const int kk = 2 * i + (lane >> 5); const int k = k0 + kk;
;         if (KS) v[i] *= (k < ksplit ? ksA[k] : ksB[k - ksplit]);
;         scr[kk * 33 + (lane & 31)] = v[i]; }
;     LDS_WAIT(); asm volatile("" ::: "memory");
;     const int c = lane & 7;
; #pragma unroll
;     for (int j = 0; j < 4; ++j) { const int n = (lane >> 3) + 8 * j; const LAS float* s = scr + (8 * c) * 33 + n;
;         v4u o; o.x = pk2(s[0 * 33], s[1 * 33]); o.y = pk2(s[2 * 33], s[3 * 33]); o.z = pk2(s[4 * 33], s[5 * 33]); o.w = pk2(s[6 * 33], s[7 * 33]);
;         *(GAS v4u*)(WT + (size_t)(n0 + n) * K + k0 + 8 * c) = o; }
;     LDS_WAIT(); asm volatile("" ::: "memory");
	s_add_u32 s6, s56, 0x1800000
	s_addc_u32 s7, s57, 0
	ds_read_b32 v226, v113
	ds_read_b32 v227, v113 offset:512
	ds_read_b32 v228, v113 offset:1024
	ds_read_b32 v229, v113 offset:1536
	ds_read_b32 v230, v113 offset:2048
	ds_read_b32 v231, v113 offset:2560
	ds_read_b32 v232, v113 offset:3072
	ds_read_b32 v233, v113 offset:3584
	s_waitcnt lgkmcnt(0)
	v_bfe_u32 v120, v226, 16, 1
	v_bfe_u32 v121, v227, 16, 1
	v_bfe_u32 v122, v228, 16, 1
	v_bfe_u32 v123, v229, 16, 1
	v_bfe_u32 v124, v230, 16, 1
	v_bfe_u32 v125, v231, 16, 1
	v_bfe_u32 v126, v232, 16, 1
	v_bfe_u32 v127, v233, 16, 1
	v_add3_u32 v226, v226, v120, s63
	v_add3_u32 v227, v227, v121, s63
	v_add3_u32 v228, v228, v122, s63
	v_add3_u32 v229, v229, v123, s63
	v_add3_u32 v230, v230, v124, s63
	v_add3_u32 v231, v231, v125, s63
	v_add3_u32 v232, v232, v126, s63
	v_add3_u32 v233, v233, v127, s63
	v_perm_b32 v242, v227, v226, s64
	v_perm_b32 v243, v229, v228, s64
	v_perm_b32 v244, v231, v230, s64
	v_perm_b32 v245, v233, v232, s64
	s_nop 0
	global_store_dwordx4 v83, v[242:245], s[6:7]
	ds_read_b32 v226, v115
	ds_read_b32 v227, v115 offset:512
	ds_read_b32 v228, v115 offset:1024
	ds_read_b32 v229, v115 offset:1536
	ds_read_b32 v230, v115 offset:2048
	ds_read_b32 v231, v115 offset:2560
	ds_read_b32 v232, v115 offset:3072
	ds_read_b32 v233, v115 offset:3584
	s_waitcnt lgkmcnt(0)
	v_bfe_u32 v120, v226, 16, 1
	v_bfe_u32 v121, v227, 16, 1
	v_bfe_u32 v122, v228, 16, 1
	v_bfe_u32 v123, v229, 16, 1
	v_bfe_u32 v124, v230, 16, 1
	v_bfe_u32 v125, v231, 16, 1
	v_bfe_u32 v126, v232, 16, 1
	v_bfe_u32 v127, v233, 16, 1
	v_add3_u32 v226, v226, v120, s63
	v_add3_u32 v227, v227, v121, s63
	v_add3_u32 v228, v228, v122, s63
	v_add3_u32 v229, v229, v123, s63
	v_add3_u32 v230, v230, v124, s63
	v_add3_u32 v231, v231, v125, s63
	v_add3_u32 v232, v232, v126, s63
	v_add3_u32 v233, v233, v127, s63
	v_perm_b32 v242, v227, v226, s64
	v_perm_b32 v243, v229, v228, s64
	v_perm_b32 v244, v231, v230, s64
	v_perm_b32 v245, v233, v232, s64
	s_nop 0
	global_store_dwordx4 v84, v[242:245], s[6:7]
	ds_read_b32 v226, v117
	ds_read_b32 v227, v117 offset:512
	ds_read_b32 v228, v117 offset:1024
	ds_read_b32 v229, v117 offset:1536
	ds_read_b32 v230, v117 offset:2048
	ds_read_b32 v231, v117 offset:2560
	ds_read_b32 v232, v117 offset:3072
	ds_read_b32 v233, v117 offset:3584
	s_waitcnt lgkmcnt(0)
	v_bfe_u32 v120, v226, 16, 1
	v_bfe_u32 v121, v227, 16, 1
	v_bfe_u32 v122, v228, 16, 1
	v_bfe_u32 v123, v229, 16, 1
	v_bfe_u32 v124, v230, 16, 1
	v_bfe_u32 v125, v231, 16, 1
	v_bfe_u32 v126, v232, 16, 1
	v_bfe_u32 v127, v233, 16, 1
	v_add3_u32 v226, v226, v120, s63
	v_add3_u32 v227, v227, v121, s63
	v_add3_u32 v228, v228, v122, s63
	v_add3_u32 v229, v229, v123, s63
	v_add3_u32 v230, v230, v124, s63
	v_add3_u32 v231, v231, v125, s63
	v_add3_u32 v232, v232, v126, s63
	v_add3_u32 v233, v233, v127, s63
	v_perm_b32 v242, v227, v226, s64
	v_perm_b32 v243, v229, v228, s64
	v_perm_b32 v244, v231, v230, s64
	v_perm_b32 v245, v233, v232, s64
	s_nop 0
	global_store_dwordx4 v85, v[242:245], s[6:7]
	ds_read_b32 v226, v119
	ds_read_b32 v227, v119 offset:512
	ds_read_b32 v228, v119 offset:1024
	ds_read_b32 v229, v119 offset:1536
	ds_read_b32 v230, v119 offset:2048
	ds_read_b32 v231, v119 offset:2560
	ds_read_b32 v232, v119 offset:3072
	ds_read_b32 v233, v119 offset:3584
	s_waitcnt lgkmcnt(0)
	v_bfe_u32 v120, v226, 16, 1
	v_bfe_u32 v121, v227, 16, 1
	v_bfe_u32 v122, v228, 16, 1
	v_bfe_u32 v123, v229, 16, 1
	v_bfe_u32 v124, v230, 16, 1
	v_bfe_u32 v125, v231, 16, 1
	v_bfe_u32 v126, v232, 16, 1
	v_bfe_u32 v127, v233, 16, 1
	v_add3_u32 v226, v226, v120, s63
	v_add3_u32 v227, v227, v121, s63
	v_add3_u32 v228, v228, v122, s63
	v_add3_u32 v229, v229, v123, s63
	v_add3_u32 v230, v230, v124, s63
	v_add3_u32 v231, v231, v125, s63
	v_add3_u32 v232, v232, v126, s63
	v_add3_u32 v233, v233, v127, s63
	v_perm_b32 v242, v227, v226, s64
	v_perm_b32 v243, v229, v228, s64
	v_perm_b32 v244, v231, v230, s64
	v_perm_b32 v245, v233, v232, s64
	s_nop 0
	global_store_dwordx4 v86, v[242:245], s[6:7]
	s_waitcnt lgkmcnt(0)
	s_barrier
; __global__ void __launch_bounds__(NWAVES * 64, 2) hybrid_fwd(Args args) {
;     ...
;     for (int L = 0; L < DEPTH; ++L) {
;         { unsigned long long wz = 0; asm volatile("" : "+s"(wz)); ws = args.ws + wz; }
;         bf16* Hres = (bf16*)(ws + WS_H);     static_assert(DEPTH == 2 && WO_F8_FROM == 1 && PROJ_F8_FROM == 1, "the phase instantiations below are written for this precision plan");
;         bf16* XN = (bf16*)(ws + WS_XN); bf16* PROJ = (bf16*)(ws + WS_PROJ); bf16* ACT = (bf16*)(ws + WS_ACT); unsigned char* CAT = (unsigned char*)(ws + WS_CAT);     const bool wo_f8 = L >= WO_F8_FROM;
;         float* ATT = (float*)(ws + WS_ATT); bf16* XBC = (bf16*)(ws + WS_XBC); bf16* Y = (bf16*)(ws + WS_Y);
;         bf16* KC = (bf16*)(ws + WS_KC); bf16* VC = (bf16*)(ws + WS_VC); float* DT = (float*)(ws + WS_DT); float* ADT = (float*)(ws + WS_ADT);
;         float* COS = (float*)(ws + WS_COS); float* SIN = (float*)(ws + WS_SIN); unsigned* BMP = (unsigned*)(ws + WS_BMP);
;         bf16* AO = (bf16*)(ws + WS_ACT);     float* STT = (float*)(ws + WS_ST); bf16* PREVB = (bf16*)(ws + WS_PREV);     float* ACSG = (float*)(ws + WS_ACSG); float* DEC = (float*)(ws + WS_DEC);
;         {
;             const bool split = (L < PROJ_F8_FROM) && (F.G == 256);
;             if (L >= PROJ_F8_FROM) { pg8::StaticOrder So; So.init(S, NPROJ, F.G, (int)blockIdx.x); pg8::Gemm g{XN, (const bf16*)(ws + WS_WIN + L * SZ_WIN), S, NPROJ, DM / 2};
;                 pg8::EpiProj E{PROJ, NPROJ, COS, SIN, QSCALE, 1.f / (XN8_SCALE * WUP8_SCALE), 0};
;                 pg8::gemm_phase<pg8::EpiProj, pg8::StaticOrder, true, true, true>(F.lds + RING_OFF, g, So, E); }
	v_readlane_b32 s12, v253, 35
	v_readlane_b32 s18, v253, 41
	v_readlane_b32 s19, v253, 42
	s_add_u32 s81, s18, 0x1f600000
	s_addc_u32 s94, s19, 0
	s_add_u32 s24, s18, 0xf600000
	v_or_b32_e32 v2, 2, v6
	v_mov_b32_e32 v3, 0x630
	v_readlane_b32 s13, v253, 36
	v_readlane_b32 s14, v253, 37
	v_readlane_b32 s15, v253, 38
	s_addc_u32 s25, s19, 0
	v_mad_u32_u24 v58, v2, s0, v3
	v_mov_b32_e32 v3, 0xc60
	s_add_u32 s26, s18, 0xb600000
	v_mad_u32_u24 v59, v2, s0, v3
	v_readlane_b32 s0, v253, 19
	s_addc_u32 s27, s19, 0
	v_readlane_b32 s2, v253, 21
	v_readlane_b32 s10, v253, 29
	v_readlane_b32 s3, v253, 22
	v_readlane_b32 s11, v253, 30
	s_add_u32 s2, s10, 0x4000000
	v_readlane_b32 s40, v253, 3
	s_addc_u32 s3, s11, 0
	v_readlane_b32 s52, v253, 15
	v_readlane_b32 s53, v253, 16
	s_add_u32 s22, s52, 0x2000
	v_readlane_b32 s8, v253, 27
	s_addc_u32 s23, s53, 0
	v_readlane_b32 s9, v253, 28
	s_add_u32 s84, s8, 0x2000
	s_addc_u32 s85, s9, 0
	s_add_u32 s33, s18, 0x200000
	v_readlane_b32 s44, v253, 7
	s_addc_u32 s38, s19, 0
	v_mov_b32_e32 v9, v11
	v_readlane_b32 s1, v253, 20
	v_readlane_b32 s45, v253, 8
	s_add_u32 s86, s44, 0xb140000
	v_mul_u32_u24_e32 v57, 0x84, v2
	v_readlane_b32 s42, v253, 5
	v_lshl_add_u64 v[2:3], s[18:19], 0, v[8:9]
	s_mov_b64 s[0:1], 0xd600000
	s_addc_u32 s87, s45, 0
	v_readlane_b32 s12, v253, 31
	v_readlane_b32 s13, v253, 32
	v_readlane_b32 s14, v253, 33
	v_readlane_b32 s15, v253, 34
	v_readlane_b32 s43, v253, 6
	v_readlane_b32 s54, v253, 17
	v_readlane_b32 s55, v253, 18
	v_lshl_add_u64 v[12:13], v[2:3], 0, s[0:1]
	s_add_u32 s88, s42, 0x4000
	s_mov_b64 s[0:1], 0x5c00000
	v_readlane_b32 s41, v253, 4
	v_readlane_b32 s46, v253, 9
	v_readlane_b32 s47, v253, 10
	v_readlane_b32 s48, v253, 11
	v_readlane_b32 s49, v253, 12
	v_readlane_b32 s50, v253, 13
	s_addc_u32 s89, s43, 0
	v_lshlrev_b32_e32 v4, 6, v18
	v_lshl_add_u64 v[14:15], v[2:3], 0, s[0:1]
	s_lshl_b32 s0, s80, 5
	s_movk_i32 s12, 0xe000
	s_movk_i32 s14, 0xe008
	s_movk_i32 s18, 0xe010
	s_movk_i32 s78, 0xe018
	s_movk_i32 s92, 0xe0d0
	s_movk_i32 s28, 0xe0d8
	s_movk_i32 s34, 0xe0e0
	s_movk_i32 s52, 0xe0e8
	s_movk_i32 s54, 0xe0f0
	s_movk_i32 s56, 0xe0f8
	v_or_b32_e32 v26, 0x2000, v18
	v_or_b32_e32 v27, 0x4000, v18
	v_or_b32_e32 v28, 0x6000, v18
	v_or_b32_e32 v29, 0x8000, v18
	v_or_b32_e32 v30, 0xa000, v18
	v_or_b32_e32 v31, 0xc000, v18
	v_or_b32_e32 v32, 0xe000, v18
	v_or_b32_e32 v33, 0x10000, v18
	v_or_b32_e32 v34, 0x12000, v18
	v_or_b32_e32 v35, 0x14000, v18
	v_or_b32_e32 v36, 0x16000, v18
	v_or_b32_e32 v37, 0x18000, v18
	v_or_b32_e32 v38, 0x1a000, v18
	v_or_b32_e32 v39, 0x1c000, v18
	v_or_b32_e32 v40, 0x1e000, v18
	v_or_b32_e32 v41, 0x20000, v18
	v_or_b32_e32 v42, 0x22000, v18
	v_or_b32_e32 v43, 0x24000, v18
	v_or_b32_e32 v44, 0x26000, v18
	v_or_b32_e32 v45, 0x28000, v18
	v_or_b32_e32 v46, 0x2a000, v18
	v_or_b32_e32 v47, 0x2c000, v18
	v_or_b32_e32 v48, 0x2e000, v18
	v_or_b32_e32 v49, 0x30000, v18
	v_or_b32_e32 v50, 0x32000, v18
	v_or_b32_e32 v51, 0x34000, v18
	v_or_b32_e32 v52, 0x36000, v18
	v_or_b32_e32 v53, 0x38000, v18
	v_or_b32_e32 v54, 0x3a000, v18
	v_or_b32_e32 v55, 0x3c000, v18
	v_or_b32_e32 v56, 0x3e000, v18
	v_and_b32_e32 v60, 64, v4
	v_mov_b32_e32 v7, v11
	s_lshl_b32 s39, s80, 6
	s_add_i32 s40, s0, 0xfff4c000
	s_lshl_b32 s41, s83, 8
	s_lshl_b32 s42, s80, 4
	s_lshl_b32 s43, s83, 7
	s_mov_b32 s91, 0
	s_mov_b32 s44, 0xc3e00000
	s_movk_i32 s45, 0x7fff
	s_mov_b32 s46, 0xffff0000
	s_movk_i32 s47, 0x2c2f
	s_movk_i32 s48, 0x2c50
	s_mov_b32 s49, 0xb140
	v_add_u32_e32 v61, 0x400, v19
	v_add_u32_e32 v62, 0x800, v19
	v_add_u32_e32 v63, 0xc00, v19
	v_mov_b32_e32 v64, 0x43e00000
	s_mov_b32 s50, s80
	s_mov_b32 s13, -1
	s_mov_b32 s15, -1
	s_mov_b32 s19, -1
	s_mov_b32 s79, -1
	s_mov_b32 s93, -1
	s_mov_b32 s29, -1
	s_mov_b32 s35, -1
	s_mov_b32 s53, -1
	s_mov_b32 s55, -1
	s_mov_b32 s57, -1
	v_readlane_b32 s16, v253, 39
	v_readlane_b32 s17, v253, 40
	v_readlane_b32 s4, v253, 23
	v_readlane_b32 s5, v253, 24
	v_readlane_b32 s6, v253, 25
	v_readlane_b32 s7, v253, 26
	v_readlane_b32 s51, v253, 14
	s_branch .LBB0_15

;     const int pr = item >> 1, kb = 2 * (pr / nblk) + (item & 1), nb = pr % nblk, k0 = 64 * kb, n0 = 32 * nb;
;     const int nr = n0 + (lane & 31); const int sc = MAP == 1 ? src_col_in(nr) : nr;
;     float v[32];
; #pragma unroll
;     for (int i = 0; i < 32; ++i) v[i] = sc >= 0 ? W[(size_t)(k0 + 2 * i + (lane >> 5)) * Nsrc + sc] : 0.f;
; #pragma unroll
;     for (int i = 0; i < 32; ++i) { const int k = k0 + 2 * i + (lane >> 5); float x = v[i] * wscale; if (KS) x *= (k < ksplit ? ksA[k] : ksB[k - ksplit]); scr[(2 * i + (lane >> 5)) * 33 + (lane & 31)] = x; }
; __global__ void __launch_bounds__(NWAVES * 64, 2) hybrid_fwd(Args args) {
;     ...
;             if (r < I_O) { if (l >= WO_F8_FROM) p0_transpose_item_f8<true>(args.in[13] + (size_t)l * DM * DM, DM, DM, DM / 32, (unsigned char*)(ws + WS_WO + l * SZ_WO), 64.f, args.in[6] + l * 2048, args.in[12] + l * 2048, 2048, scr, r, lane);
;                 else p0_transpose_item<0, true>(args.in[13] + (size_t)l * DM * DM, DM, DM, DM / 32, (bf16*)(ws + WS_WO + l * SZ_WO), args.in[6] + l * 2048, args.in[12] + l * 2048, 2048, scr, r, lane); continue; } r -= I_O;
;             if (r < I_UP) { p0_transpose_item_f8<true>(args.in[15] + (size_t)l * DM * FF, DM, FF, FF / 32, (unsigned char*)(ws + WS_WUP + l * SZ_WUP), WUP8_SCALE, args.in[14] + l * DM, args.in[14] + l * DM, DM, scr, r, lane); continue; } r -= I_UP;
;             p0_transpose_item_f8<false>(args.in[16] + (size_t)l * FF * DM, FF, DM, DM / 32, (unsigned char*)(ws + WS_WDN + l * SZ_WDN), 128.f, args.in[16], args.in[16], 0, scr, r, lane);
.LBB0_575:
	s_waitcnt vmcnt(0)
	s_barrier
	s_cmpk_lt_u32 s77, 0xa0
	s_cbranch_scc1 .Llite_skip
	s_sub_i32 s16, s77, 160
	v_and_b32_e32 v17, 63, v0
	v_lshrrev_b32_e32 v18, 6, v0
	v_lshrrev_b32_e32 v14, 5, v17
	v_lshl_add_u32 v15, v18, 4, v14
	v_and_b32_e32 v16, 31, v17
	v_xor_b32_e32 v16, v16, v18
	v_lshlrev_b32_e32 v16, 4, v16
	v_lshl_add_u32 v4, v15, 9, v16
	v_add_u32_e32 v5, 0x10000, v4
	v_and_b32_e32 v16, 31, v17
	v_lshlrev_b32_e32 v16, 4, v16
	s_mov_b32 s21, 0x4000
	v_mad_u32_u24 v10, v15, s21, v16
	v_and_b32_e32 v14, 7, v17
	v_lshrrev_b32_e32 v15, 5, v17
	v_lshl_add_u32 v15, v18, 2, v15
	v_xor_b32_e32 v15, v15, v14
	v_lshlrev_b32_e32 v15, 4, v15
	v_lshl_add_u32 v15, v14, 13, v15
	v_bfe_u32 v16, v17, 3, 2
	v_lshl_add_u32 v6, v16, 2, v15
	v_add_u32_e32 v7, 0x10000, v6
	v_and_b32_e32 v14, 7, v17
	v_lshrrev_b32_e32 v15, 5, v17
	v_lshl_add_u32 v15, v18, 2, v15
	v_add_u32_e32 v15, 2, v15
	v_xor_b32_e32 v15, v15, v14
	v_lshlrev_b32_e32 v15, 4, v15
	v_lshl_add_u32 v15, v14, 13, v15
	v_bfe_u32 v16, v17, 3, 2
	v_lshl_add_u32 v8, v16, 2, v15
	v_add_u32_e32 v9, 0x10000, v8
	v_lshrrev_b32_e32 v14, 3, v17
	v_lshl_add_u32 v14, v18, 4, v14
	v_and_b32_e32 v15, 7, v17
	v_lshlrev_b32_e32 v15, 4, v15
	v_lshl_add_u32 v11, v14, 14, v15
	v_lshrrev_b32_e32 v14, 3, v17
	v_lshl_add_u32 v14, v18, 4, v14
	v_add_u32_e32 v14, 8, v14
	v_and_b32_e32 v15, 7, v17
	v_lshlrev_b32_e32 v15, 4, v15
	v_lshl_add_u32 v12, v14, 14, v15
	v_mov_b32_e32 v13, 0x43e00000
	s_mov_b32 s20, 0xc3e00000
	v_readlane_b32 s2, v253, 35
	v_readlane_b32 s3, v253, 36
	v_readlane_b32 s4, v253, 41
	v_readlane_b32 s5, v253, 42
	s_add_u32 s2, s2, 0x10000000
	s_addc_u32 s3, s3, 0
	s_add_u32 s4, s4, 0x27600000
	s_addc_u32 s5, s5, 0
	s_and_b32 s38, s16, 31
	s_lshr_b32 s39, s16, 5
	v_lshrrev_b32_e32 v14, 5, v17
	v_lshl_add_u32 v15, v18, 4, v14
	v_lshlrev_b32_e32 v19, 2, v15
	v_lshrrev_b32_e32 v14, 3, v17
	v_lshl_add_u32 v14, v18, 4, v14
	v_and_b32_e32 v15, 7, v17
	v_lshlrev_b32_e32 v15, 4, v15
	v_lshl_add_u32 v28, v14, 12, v15
	v_lshrrev_b32_e32 v14, 3, v17
	v_lshl_add_u32 v14, v18, 4, v14
	v_add_u32_e32 v14, 8, v14
	v_and_b32_e32 v15, 7, v17
	v_lshlrev_b32_e32 v15, 4, v15
	v_lshl_add_u32 v29, v14, 12, v15
	v_readlane_b32 s0, v253, 15
	v_readlane_b32 s1, v253, 16
	v_readlane_b32 s22, v253, 27
	v_readlane_b32 s23, v253, 28
	s_sub_i32 s45, s38, 16
	s_cmp_lt_u32 s38, 16
	s_cselect_b32 s0, s0, s22
	s_cselect_b32 s1, s1, s23
	s_cselect_b32 s45, s38, s45
	s_lshl_b32 s45, s45, 9
	s_add_i32 s45, s45, 0x2000
	s_add_u32 s0, s0, s45
	s_addc_u32 s1, s1, 0
	global_load_dword v20, v19, s[0:1] offset:0
	global_load_dword v21, v19, s[0:1] offset:8
	global_load_dword v22, v19, s[0:1] offset:16
	global_load_dword v23, v19, s[0:1] offset:24
	global_load_dword v24, v19, s[0:1] offset:32
	global_load_dword v25, v19, s[0:1] offset:40
	global_load_dword v26, v19, s[0:1] offset:48
	global_load_dword v27, v19, s[0:1] offset:56
	s_waitcnt vmcnt(0)
	v_mul_f32_e32 v20, 0x42800000, v20
	v_mul_f32_e32 v21, 0x42800000, v21
	v_mul_f32_e32 v22, 0x42800000, v22
	v_mul_f32_e32 v23, 0x42800000, v23
	v_mul_f32_e32 v24, 0x42800000, v24
	v_mul_f32_e32 v25, 0x42800000, v25
	v_mul_f32_e32 v26, 0x42800000, v26
	v_mul_f32_e32 v27, 0x42800000, v27
	v_readlane_b32 s22, v253, 29
	v_readlane_b32 s23, v253, 30
	s_add_u32 s22, s22, 0x4000000
	s_addc_u32 s23, s23, 0
	s_lshl_b32 s45, s38, 21
	s_add_u32 s22, s22, s45
	s_addc_u32 s23, s23, 0
	v_readlane_b32 s50, v253, 41
	v_readlane_b32 s51, v253, 42
	s_add_u32 s50, s50, 0xd600000
	s_addc_u32 s51, s51, 0
	s_lshl_b32 s45, s38, 7
	s_add_u32 s50, s50, s45
	s_addc_u32 s51, s51, 0
	s_mov_b32 s45, 0x10000
	v_lshrrev_b32_e32 v14, 5, v17
	v_lshl_add_u32 v15, v18, 4, v14
	v_and_b32_e32 v16, 31, v17
	v_lshlrev_b32_e32 v16, 4, v16
	v_mad_u32_u24 v30, v15, s45, v16
	v_readlane_b32 s0, v253, 31
	v_readlane_b32 s1, v253, 32
	s_lshl_b32 s45, s38, 9
	s_add_i32 s45, s45, 0x4000
	s_add_u32 s0, s0, s45
	s_addc_u32 s1, s1, 0
	global_load_dword v232, v19, s[0:1] offset:0
	global_load_dword v233, v19, s[0:1] offset:8
	global_load_dword v234, v19, s[0:1] offset:16
	global_load_dword v235, v19, s[0:1] offset:24
	global_load_dword v236, v19, s[0:1] offset:32
	global_load_dword v237, v19, s[0:1] offset:40
	global_load_dword v238, v19, s[0:1] offset:48
	global_load_dword v239, v19, s[0:1] offset:56
	s_waitcnt vmcnt(0)
; #define LDS_WAIT() asm volatile("s_waitcnt lgkmcnt(0)" ::: "memory")
;     ...
;     for (int i = 0; i < 32; ++i) v[i] = sc >= 0 ? W[(size_t)(k0 + 2 * i + (lane >> 5)) * Nsrc + sc] : 0.f;
; #pragma unroll
;     for (int i = 0; i < 32; ++i) { const int k = k0 + 2 * i + (lane >> 5); float x = v[i] * wscale; if (KS) x *= (k < ksplit ? ksA[k] : ksB[k - ksplit]); scr[(2 * i + (lane >> 5)) * 33 + (lane & 31)] = x; }
;     LDS_WAIT(); asm volatile("" ::: "memory");
; __global__ void __launch_bounds__(NWAVES * 64, 2) hybrid_fwd(Args args) {
;     ...
;             if (r < I_UP) { p0_transpose_item_f8<true>(args.in[15] + (size_t)l * DM * FF, DM, FF, FF / 32, (unsigned char*)(ws + WS_WUP + l * SZ_WUP), WUP8_SCALE, args.in[14] + l * DM, args.in[14] + l * DM, DM, scr, r, lane); continue; } r -= I_UP;
;             p0_transpose_item_f8<false>(args.in[16] + (size_t)l * FF * DM, FF, DM, DM / 32, (unsigned char*)(ws + WS_WDN + l * SZ_WDN), 128.f, args.in[16], args.in[16], 0, scr, r, lane);
	v_mul_f32_e32 v232, 0x42800000, v232
	v_mul_f32_e32 v233, 0x42800000, v233
	v_mul_f32_e32 v234, 0x42800000, v234
	v_mul_f32_e32 v235, 0x42800000, v235
	v_mul_f32_e32 v236, 0x42800000, v236
	v_mul_f32_e32 v237, 0x42800000, v237
	v_mul_f32_e32 v238, 0x42800000, v238
	v_mul_f32_e32 v239, 0x42800000, v239
	v_readlane_b32 s46, v253, 33
	v_readlane_b32 s47, v253, 34
	s_add_u32 s46, s46, 0x10000000
	s_addc_u32 s47, s47, 0
	s_lshl_b32 s45, s38, 23
	s_add_u32 s46, s46, s45
	s_addc_u32 s47, s47, 0
	v_readlane_b32 s64, v253, 41
	v_readlane_b32 s65, v253, 42
	s_add_u32 s64, s64, 0x17600000
	s_addc_u32 s65, s65, 0
	s_lshl_b32 s45, s38, 7
	s_add_u32 s64, s64, s45
	s_addc_u32 s65, s65, 0
	s_add_i32 s17, s16, 0
	s_min_u32 s17, s17, 0xfff
	s_lshr_b32 s18, s17, 5
	s_add_i32 s18, s18, 0
	s_and_b32 s19, s17, 31
	s_lshl_b32 s18, s18, 21
	s_lshl_b32 s19, s19, 9
	s_add_u32 s18, s18, s19
	s_add_u32 s12, s2, s18
	s_addc_u32 s13, s3, 0
	global_load_dwordx4 v[36:39], v10, s[12:13]
	s_add_u32 s12, s12, 0x8000
	s_addc_u32 s13, s13, 0
	global_load_dwordx4 v[40:43], v10, s[12:13]
	s_add_u32 s12, s12, 0x8000
	s_addc_u32 s13, s13, 0
	global_load_dwordx4 v[44:47], v10, s[12:13]
	s_add_u32 s12, s12, 0x8000
	s_addc_u32 s13, s13, 0
	global_load_dwordx4 v[48:51], v10, s[12:13]
	s_add_u32 s12, s12, 0x8000
	s_addc_u32 s13, s13, 0
	global_load_dwordx4 v[52:55], v10, s[12:13]
	s_add_u32 s12, s12, 0x8000
	s_addc_u32 s13, s13, 0
	global_load_dwordx4 v[56:59], v10, s[12:13]
	s_add_u32 s12, s12, 0x8000
	s_addc_u32 s13, s13, 0
	global_load_dwordx4 v[60:63], v10, s[12:13]
	s_add_u32 s12, s12, 0x8000
	s_addc_u32 s13, s13, 0
	global_load_dwordx4 v[64:67], v10, s[12:13]
	s_add_i32 s17, s16, 96
	s_min_u32 s17, s17, 0xfff
	s_lshr_b32 s18, s17, 5
	s_add_i32 s18, s18, 0
	s_and_b32 s19, s17, 31
	s_lshl_b32 s18, s18, 21
	s_lshl_b32 s19, s19, 9
	s_add_u32 s18, s18, s19
	s_add_u32 s12, s2, s18
	s_addc_u32 s13, s3, 0
	global_load_dwordx4 v[68:71], v10, s[12:13]
	s_add_u32 s12, s12, 0x8000
	s_addc_u32 s13, s13, 0
	global_load_dwordx4 v[72:75], v10, s[12:13]
	s_add_u32 s12, s12, 0x8000
	s_addc_u32 s13, s13, 0
	global_load_dwordx4 v[76:79], v10, s[12:13]
	s_add_u32 s12, s12, 0x8000
	s_addc_u32 s13, s13, 0
	global_load_dwordx4 v[80:83], v10, s[12:13]
	s_add_u32 s12, s12, 0x8000
	s_addc_u32 s13, s13, 0
	global_load_dwordx4 v[84:87], v10, s[12:13]
	s_add_u32 s12, s12, 0x8000
	s_addc_u32 s13, s13, 0
	global_load_dwordx4 v[88:91], v10, s[12:13]
	s_add_u32 s12, s12, 0x8000
	s_addc_u32 s13, s13, 0
	global_load_dwordx4 v[92:95], v10, s[12:13]
	s_add_u32 s12, s12, 0x8000
	s_addc_u32 s13, s13, 0
	global_load_dwordx4 v[96:99], v10, s[12:13]
	s_add_i32 s17, s16, 192
	s_min_u32 s17, s17, 0xfff
	s_lshr_b32 s18, s17, 5
	s_add_i32 s18, s18, 0
	s_and_b32 s19, s17, 31
	s_lshl_b32 s18, s18, 21
	s_lshl_b32 s19, s19, 9
	s_add_u32 s18, s18, s19
	s_add_u32 s12, s2, s18
	s_addc_u32 s13, s3, 0
	global_load_dwordx4 v[100:103], v10, s[12:13]
	s_add_u32 s12, s12, 0x8000
	s_addc_u32 s13, s13, 0
	global_load_dwordx4 v[104:107], v10, s[12:13]
	s_add_u32 s12, s12, 0x8000
	s_addc_u32 s13, s13, 0
	global_load_dwordx4 v[108:111], v10, s[12:13]
	s_add_u32 s12, s12, 0x8000
	s_addc_u32 s13, s13, 0
	global_load_dwordx4 v[112:115], v10, s[12:13]
	s_add_u32 s12, s12, 0x8000
	s_addc_u32 s13, s13, 0
	global_load_dwordx4 v[116:119], v10, s[12:13]
	s_add_u32 s12, s12, 0x8000
	s_addc_u32 s13, s13, 0
	global_load_dwordx4 v[120:123], v10, s[12:13]
	s_add_u32 s12, s12, 0x8000
	s_addc_u32 s13, s13, 0
	global_load_dwordx4 v[124:127], v10, s[12:13]
	s_add_u32 s12, s12, 0x8000
	s_addc_u32 s13, s13, 0
	global_load_dwordx4 v[128:131], v10, s[12:13]
	s_add_i32 s17, s16, 288
	s_min_u32 s17, s17, 0xfff
	s_lshr_b32 s18, s17, 5
	s_add_i32 s18, s18, 0
	s_and_b32 s19, s17, 31
	s_lshl_b32 s18, s18, 21
	s_lshl_b32 s19, s19, 9
	s_add_u32 s18, s18, s19
	s_add_u32 s12, s2, s18
	s_addc_u32 s13, s3, 0
	global_load_dwordx4 v[132:135], v10, s[12:13]
	s_add_u32 s12, s12, 0x8000
	s_addc_u32 s13, s13, 0
	global_load_dwordx4 v[136:139], v10, s[12:13]
	s_add_u32 s12, s12, 0x8000
	s_addc_u32 s13, s13, 0
	global_load_dwordx4 v[140:143], v10, s[12:13]
	s_add_u32 s12, s12, 0x8000
	s_addc_u32 s13, s13, 0
	global_load_dwordx4 v[144:147], v10, s[12:13]
	s_add_u32 s12, s12, 0x8000
	s_addc_u32 s13, s13, 0
	global_load_dwordx4 v[148:151], v10, s[12:13]
	s_add_u32 s12, s12, 0x8000
	s_addc_u32 s13, s13, 0
	global_load_dwordx4 v[152:155], v10, s[12:13]
	s_add_u32 s12, s12, 0x8000
	s_addc_u32 s13, s13, 0
	global_load_dwordx4 v[156:159], v10, s[12:13]
	s_add_u32 s12, s12, 0x8000
	s_addc_u32 s13, s13, 0
	global_load_dwordx4 v[160:163], v10, s[12:13]
	s_waitcnt vmcnt(24)
	v_mul_f32_e32 v36, 0x43000000, v36
	v_mul_f32_e32 v37, 0x43000000, v37
	v_mul_f32_e32 v38, 0x43000000, v38
	v_mul_f32_e32 v39, 0x43000000, v39
	ds_write_b128 v4, v[36:39]
	v_mul_f32_e32 v40, 0x43000000, v40
	v_mul_f32_e32 v41, 0x43000000, v41
	v_mul_f32_e32 v42, 0x43000000, v42
	v_mul_f32_e32 v43, 0x43000000, v43
	ds_write_b128 v4, v[40:43] offset:1024
	v_mul_f32_e32 v44, 0x43000000, v44
	v_mul_f32_e32 v45, 0x43000000, v45
	v_mul_f32_e32 v46, 0x43000000, v46
	v_mul_f32_e32 v47, 0x43000000, v47
	ds_write_b128 v4, v[44:47] offset:2048
	v_mul_f32_e32 v48, 0x43000000, v48
	v_mul_f32_e32 v49, 0x43000000, v49
	v_mul_f32_e32 v50, 0x43000000, v50
	v_mul_f32_e32 v51, 0x43000000, v51
	ds_write_b128 v4, v[48:51] offset:3072
	v_mul_f32_e32 v52, 0x43000000, v52
	v_mul_f32_e32 v53, 0x43000000, v53
	v_mul_f32_e32 v54, 0x43000000, v54
	v_mul_f32_e32 v55, 0x43000000, v55
	ds_write_b128 v4, v[52:55] offset:4096
	v_mul_f32_e32 v56, 0x43000000, v56
	v_mul_f32_e32 v57, 0x43000000, v57
	v_mul_f32_e32 v58, 0x43000000, v58
	v_mul_f32_e32 v59, 0x43000000, v59
	ds_write_b128 v4, v[56:59] offset:5120
	v_mul_f32_e32 v60, 0x43000000, v60
	v_mul_f32_e32 v61, 0x43000000, v61
	v_mul_f32_e32 v62, 0x43000000, v62
	v_mul_f32_e32 v63, 0x43000000, v63
	ds_write_b128 v4, v[60:63] offset:6144
	v_mul_f32_e32 v64, 0x43000000, v64
	v_mul_f32_e32 v65, 0x43000000, v65
	v_mul_f32_e32 v66, 0x43000000, v66
	v_mul_f32_e32 v67, 0x43000000, v67
	ds_write_b128 v4, v[64:67] offset:7168
	s_waitcnt lgkmcnt(0)
	s_barrier
; #define GAS __attribute__((address_space(1)))
; #define LAS __attribute__((address_space(3)))
; #define LDS_WAIT() asm volatile("s_waitcnt lgkmcnt(0)" ::: "memory")
;     ...
;     for (int i = 0; i < 32; ++i) v[i] = sc >= 0 ? W[(size_t)(k0 + 2 * i + (lane >> 5)) * Nsrc + sc] : 0.f;
; #pragma unroll
;     for (int i = 0; i < 32; ++i) { const int k = k0 + 2 * i + (lane >> 5); float x = v[i] * wscale; if (KS) x *= (k < ksplit ? ksA[k] : ksB[k - ksplit]); scr[(2 * i + (lane >> 5)) * 33 + (lane & 31)] = x; }
;     LDS_WAIT(); asm volatile("" ::: "memory");
;     const int c = lane & 7;
; #pragma unroll
;     for (int j = 0; j < 4; ++j) { const int n = (lane >> 3) + 8 * j; const LAS float* s = scr + (8 * c) * 33 + n;
;         const unsigned long long o = (unsigned long long)pg8::pk4_fp8(s[0 * 33], s[1 * 33], s[2 * 33], s[3 * 33]) | ((unsigned long long)pg8::pk4_fp8(s[4 * 33], s[5 * 33], s[6 * 33], s[7 * 33]) << 32);
;         *(GAS unsigned long long*)(WT + (size_t)(n0 + n) * K + k0 + 8 * c) = o; }
	s_add_i32 s17, s16, 384
	s_min_u32 s17, s17, 0xfff
	s_lshr_b32 s18, s17, 5
	s_add_i32 s18, s18, 0
	s_and_b32 s19, s17, 31
	s_lshl_b32 s18, s18, 21
	s_lshl_b32 s19, s19, 9
	s_add_u32 s18, s18, s19
	s_add_u32 s12, s2, s18
	s_addc_u32 s13, s3, 0
	global_load_dwordx4 v[36:39], v10, s[12:13]
	s_add_u32 s12, s12, 0x8000
	s_addc_u32 s13, s13, 0
	global_load_dwordx4 v[40:43], v10, s[12:13]
	s_add_u32 s12, s12, 0x8000
	s_addc_u32 s13, s13, 0
	global_load_dwordx4 v[44:47], v10, s[12:13]
	s_add_u32 s12, s12, 0x8000
	s_addc_u32 s13, s13, 0
	global_load_dwordx4 v[48:51], v10, s[12:13]
	s_add_u32 s12, s12, 0x8000
	s_addc_u32 s13, s13, 0
	global_load_dwordx4 v[52:55], v10, s[12:13]
	s_add_u32 s12, s12, 0x8000
	s_addc_u32 s13, s13, 0
	global_load_dwordx4 v[56:59], v10, s[12:13]
	s_add_u32 s12, s12, 0x8000
	s_addc_u32 s13, s13, 0
	global_load_dwordx4 v[60:63], v10, s[12:13]
	s_add_u32 s12, s12, 0x8000
	s_addc_u32 s13, s13, 0
	global_load_dwordx4 v[64:67], v10, s[12:13]
	s_add_i32 s17, s16, 0
	s_min_u32 s17, s17, 0xfff
	s_lshr_b32 s18, s17, 5
	s_add_i32 s18, s18, 0
	s_and_b32 s19, s17, 31
	s_lshl_b32 s19, s19, 21
	s_lshl_b32 s18, s18, 7
	s_add_u32 s18, s18, s19
	s_add_u32 s14, s4, s18
	s_addc_u32 s15, s5, 0
	ds_read_b32 v170, v6
	ds_read_b32 v171, v6 offset:512
	ds_read_b32 v172, v6 offset:1024
	ds_read_b32 v173, v6 offset:1536
	ds_read_b32 v174, v6 offset:2048
	ds_read_b32 v175, v6 offset:2560
	ds_read_b32 v176, v6 offset:3072
	ds_read_b32 v177, v6 offset:3584
	ds_read_b32 v196, v6 offset:4096
	ds_read_b32 v197, v6 offset:4608
	ds_read_b32 v198, v6 offset:5120
	ds_read_b32 v199, v6 offset:5632
	ds_read_b32 v200, v6 offset:6144
	ds_read_b32 v201, v6 offset:6656
	ds_read_b32 v202, v6 offset:7168
	ds_read_b32 v203, v6 offset:7680
	s_waitcnt lgkmcnt(0)
	v_max_f32_e32 v170, v170, v170
	v_max_f32_e32 v171, v171, v171
	v_max_f32_e32 v172, v172, v172
	v_max_f32_e32 v173, v173, v173
	v_max_f32_e32 v174, v174, v174
	v_max_f32_e32 v175, v175, v175
	v_max_f32_e32 v176, v176, v176
	v_max_f32_e32 v177, v177, v177
	v_max_f32_e32 v196, v196, v196
	v_max_f32_e32 v197, v197, v197
	v_max_f32_e32 v198, v198, v198
	v_max_f32_e32 v199, v199, v199
	v_max_f32_e32 v200, v200, v200
	v_max_f32_e32 v201, v201, v201
	v_max_f32_e32 v202, v202, v202
	v_max_f32_e32 v203, v203, v203
	v_med3_f32 v170, v170, s20, v13
	v_med3_f32 v171, v171, s20, v13
	v_med3_f32 v172, v172, s20, v13
	v_med3_f32 v173, v173, s20, v13
	v_med3_f32 v174, v174, s20, v13
	v_med3_f32 v175, v175, s20, v13
	v_med3_f32 v176, v176, s20, v13
	v_med3_f32 v177, v177, s20, v13
	v_med3_f32 v196, v196, s20, v13
	v_med3_f32 v197, v197, s20, v13
	v_med3_f32 v198, v198, s20, v13
	v_med3_f32 v199, v199, s20, v13
	v_med3_f32 v200, v200, s20, v13
	v_med3_f32 v201, v201, s20, v13
	v_med3_f32 v202, v202, s20, v13
	v_med3_f32 v203, v203, s20, v13
	v_mov_b32_e32 v208, 0
	v_mov_b32_e32 v209, 0
	v_mov_b32_e32 v210, 0
	v_mov_b32_e32 v211, 0
	v_cvt_pk_fp8_f32 v208, v170, v171
	v_cvt_pk_fp8_f32 v209, v174, v175
	v_cvt_pk_fp8_f32 v210, v196, v197
	v_cvt_pk_fp8_f32 v211, v200, v201
	v_cvt_pk_fp8_f32 v208, v172, v173 op_sel:[0,0,1]
	v_cvt_pk_fp8_f32 v209, v176, v177 op_sel:[0,0,1]
	v_cvt_pk_fp8_f32 v210, v198, v199 op_sel:[0,0,1]
	v_cvt_pk_fp8_f32 v211, v202, v203 op_sel:[0,0,1]
	s_nop 0
	global_store_dwordx4 v11, v[208:211], s[14:15]
	ds_read_b32 v170, v8
	ds_read_b32 v171, v8 offset:512
	ds_read_b32 v172, v8 offset:1024
	ds_read_b32 v173, v8 offset:1536
	ds_read_b32 v174, v8 offset:2048
	ds_read_b32 v175, v8 offset:2560
	ds_read_b32 v176, v8 offset:3072
	ds_read_b32 v177, v8 offset:3584
	ds_read_b32 v196, v8 offset:4096
	ds_read_b32 v197, v8 offset:4608
	ds_read_b32 v198, v8 offset:5120
	ds_read_b32 v199, v8 offset:5632
	ds_read_b32 v200, v8 offset:6144
	ds_read_b32 v201, v8 offset:6656
	ds_read_b32 v202, v8 offset:7168
	ds_read_b32 v203, v8 offset:7680
	s_waitcnt lgkmcnt(0)
	v_max_f32_e32 v170, v170, v170
	v_max_f32_e32 v171, v171, v171
	v_max_f32_e32 v172, v172, v172
	v_max_f32_e32 v173, v173, v173
	v_max_f32_e32 v174, v174, v174
	v_max_f32_e32 v175, v175, v175
	v_max_f32_e32 v176, v176, v176
	v_max_f32_e32 v177, v177, v177
	v_max_f32_e32 v196, v196, v196
	v_max_f32_e32 v197, v197, v197
	v_max_f32_e32 v198, v198, v198
	v_max_f32_e32 v199, v199, v199
	v_max_f32_e32 v200, v200, v200
	v_max_f32_e32 v201, v201, v201
	v_max_f32_e32 v202, v202, v202
	v_max_f32_e32 v203, v203, v203
	v_med3_f32 v170, v170, s20, v13
	v_med3_f32 v171, v171, s20, v13
	v_med3_f32 v172, v172, s20, v13
	v_med3_f32 v173, v173, s20, v13
	v_med3_f32 v174, v174, s20, v13
	v_med3_f32 v175, v175, s20, v13
	v_med3_f32 v176, v176, s20, v13
	v_med3_f32 v177, v177, s20, v13
	v_med3_f32 v196, v196, s20, v13
	v_med3_f32 v197, v197, s20, v13
	v_med3_f32 v198, v198, s20, v13
	v_med3_f32 v199, v199, s20, v13
	v_med3_f32 v200, v200, s20, v13
	v_med3_f32 v201, v201, s20, v13
	v_med3_f32 v202, v202, s20, v13
	v_med3_f32 v203, v203, s20, v13
	v_mov_b32_e32 v208, 0
	v_mov_b32_e32 v209, 0
	v_mov_b32_e32 v210, 0
	v_mov_b32_e32 v211, 0
	v_cvt_pk_fp8_f32 v208, v170, v171
	v_cvt_pk_fp8_f32 v209, v174, v175
	v_cvt_pk_fp8_f32 v210, v196, v197
	v_cvt_pk_fp8_f32 v211, v200, v201
	v_cvt_pk_fp8_f32 v208, v172, v173 op_sel:[0,0,1]
	v_cvt_pk_fp8_f32 v209, v176, v177 op_sel:[0,0,1]
	v_cvt_pk_fp8_f32 v210, v198, v199 op_sel:[0,0,1]
	v_cvt_pk_fp8_f32 v211, v202, v203 op_sel:[0,0,1]
	s_nop 0
	global_store_dwordx4 v12, v[208:211], s[14:15]
	s_waitcnt vmcnt(26)
	v_mul_f32_e32 v68, 0x43000000, v68
	v_mul_f32_e32 v69, 0x43000000, v69
	v_mul_f32_e32 v70, 0x43000000, v70
	v_mul_f32_e32 v71, 0x43000000, v71
	ds_write_b128 v5, v[68:71]
	v_mul_f32_e32 v72, 0x43000000, v72
	v_mul_f32_e32 v73, 0x43000000, v73
	v_mul_f32_e32 v74, 0x43000000, v74
	v_mul_f32_e32 v75, 0x43000000, v75
	ds_write_b128 v5, v[72:75] offset:1024
	v_mul_f32_e32 v76, 0x43000000, v76
	v_mul_f32_e32 v77, 0x43000000, v77
	v_mul_f32_e32 v78, 0x43000000, v78
	v_mul_f32_e32 v79, 0x43000000, v79
	ds_write_b128 v5, v[76:79] offset:2048
	v_mul_f32_e32 v80, 0x43000000, v80
	v_mul_f32_e32 v81, 0x43000000, v81
	v_mul_f32_e32 v82, 0x43000000, v82
	v_mul_f32_e32 v83, 0x43000000, v83
	ds_write_b128 v5, v[80:83] offset:3072
	v_mul_f32_e32 v84, 0x43000000, v84
	v_mul_f32_e32 v85, 0x43000000, v85
	v_mul_f32_e32 v86, 0x43000000, v86
	v_mul_f32_e32 v87, 0x43000000, v87
	ds_write_b128 v5, v[84:87] offset:4096
	v_mul_f32_e32 v88, 0x43000000, v88
	v_mul_f32_e32 v89, 0x43000000, v89
	v_mul_f32_e32 v90, 0x43000000, v90
	v_mul_f32_e32 v91, 0x43000000, v91
	ds_write_b128 v5, v[88:91] offset:5120
	v_mul_f32_e32 v92, 0x43000000, v92
	v_mul_f32_e32 v93, 0x43000000, v93
	v_mul_f32_e32 v94, 0x43000000, v94
	v_mul_f32_e32 v95, 0x43000000, v95
	ds_write_b128 v5, v[92:95] offset:6144
	v_mul_f32_e32 v96, 0x43000000, v96
	v_mul_f32_e32 v97, 0x43000000, v97
	v_mul_f32_e32 v98, 0x43000000, v98
	v_mul_f32_e32 v99, 0x43000000, v99
	ds_write_b128 v5, v[96:99] offset:7168
	s_waitcnt lgkmcnt(0)
	s_barrier
; #define GAS __attribute__((address_space(1)))
; #define LAS __attribute__((address_space(3)))
; #define LDS_WAIT() asm volatile("s_waitcnt lgkmcnt(0)" ::: "memory")
;     ...
;     for (int i = 0; i < 32; ++i) v[i] = sc >= 0 ? W[(size_t)(k0 + 2 * i + (lane >> 5)) * Nsrc + sc] : 0.f;
; #pragma unroll
;     for (int i = 0; i < 32; ++i) { const int k = k0 + 2 * i + (lane >> 5); float x = v[i] * wscale; if (KS) x *= (k < ksplit ? ksA[k] : ksB[k - ksplit]); scr[(2 * i + (lane >> 5)) * 33 + (lane & 31)] = x; }
;     LDS_WAIT(); asm volatile("" ::: "memory");
;     const int c = lane & 7;
; #pragma unroll
;     for (int j = 0; j < 4; ++j) { const int n = (lane >> 3) + 8 * j; const LAS float* s = scr + (8 * c) * 33 + n;
;         const unsigned long long o = (unsigned long long)pg8::pk4_fp8(s[0 * 33], s[1 * 33], s[2 * 33], s[3 * 33]) | ((unsigned long long)pg8::pk4_fp8(s[4 * 33], s[5 * 33], s[6 * 33], s[7 * 33]) << 32);
;         *(GAS unsigned long long*)(WT + (size_t)(n0 + n) * K + k0 + 8 * c) = o; }
	s_add_i32 s17, s16, 480
	s_min_u32 s17, s17, 0xfff
	s_lshr_b32 s18, s17, 5
	s_add_i32 s18, s18, 0
	s_and_b32 s19, s17, 31
	s_lshl_b32 s18, s18, 21
	s_lshl_b32 s19, s19, 9
	s_add_u32 s18, s18, s19
	s_add_u32 s12, s2, s18
	s_addc_u32 s13, s3, 0
	global_load_dwordx4 v[68:71], v10, s[12:13]
	s_add_u32 s12, s12, 0x8000
	s_addc_u32 s13, s13, 0
	global_load_dwordx4 v[72:75], v10, s[12:13]
	s_add_u32 s12, s12, 0x8000
	s_addc_u32 s13, s13, 0
	global_load_dwordx4 v[76:79], v10, s[12:13]
	s_add_u32 s12, s12, 0x8000
	s_addc_u32 s13, s13, 0
	global_load_dwordx4 v[80:83], v10, s[12:13]
	s_add_u32 s12, s12, 0x8000
	s_addc_u32 s13, s13, 0
	global_load_dwordx4 v[84:87], v10, s[12:13]
	s_add_u32 s12, s12, 0x8000
	s_addc_u32 s13, s13, 0
	global_load_dwordx4 v[88:91], v10, s[12:13]
	s_add_u32 s12, s12, 0x8000
	s_addc_u32 s13, s13, 0
	global_load_dwordx4 v[92:95], v10, s[12:13]
	s_add_u32 s12, s12, 0x8000
	s_addc_u32 s13, s13, 0
	global_load_dwordx4 v[96:99], v10, s[12:13]
	s_add_i32 s17, s16, 96
	s_min_u32 s17, s17, 0xfff
	s_lshr_b32 s18, s17, 5
	s_add_i32 s18, s18, 0
	s_and_b32 s19, s17, 31
	s_lshl_b32 s19, s19, 21
	s_lshl_b32 s18, s18, 7
	s_add_u32 s18, s18, s19
	s_add_u32 s14, s4, s18
	s_addc_u32 s15, s5, 0
	ds_read_b32 v170, v7
	ds_read_b32 v171, v7 offset:512
	ds_read_b32 v172, v7 offset:1024
	ds_read_b32 v173, v7 offset:1536
	ds_read_b32 v174, v7 offset:2048
	ds_read_b32 v175, v7 offset:2560
	ds_read_b32 v176, v7 offset:3072
	ds_read_b32 v177, v7 offset:3584
	ds_read_b32 v196, v7 offset:4096
	ds_read_b32 v197, v7 offset:4608
	ds_read_b32 v198, v7 offset:5120
	ds_read_b32 v199, v7 offset:5632
	ds_read_b32 v200, v7 offset:6144
	ds_read_b32 v201, v7 offset:6656
	ds_read_b32 v202, v7 offset:7168
	ds_read_b32 v203, v7 offset:7680
	s_waitcnt lgkmcnt(0)
	v_max_f32_e32 v170, v170, v170
	v_max_f32_e32 v171, v171, v171
	v_max_f32_e32 v172, v172, v172
	v_max_f32_e32 v173, v173, v173
	v_max_f32_e32 v174, v174, v174
	v_max_f32_e32 v175, v175, v175
	v_max_f32_e32 v176, v176, v176
	v_max_f32_e32 v177, v177, v177
	v_max_f32_e32 v196, v196, v196
	v_max_f32_e32 v197, v197, v197
	v_max_f32_e32 v198, v198, v198
	v_max_f32_e32 v199, v199, v199
	v_max_f32_e32 v200, v200, v200
	v_max_f32_e32 v201, v201, v201
	v_max_f32_e32 v202, v202, v202
	v_max_f32_e32 v203, v203, v203
	v_med3_f32 v170, v170, s20, v13
	v_med3_f32 v171, v171, s20, v13
	v_med3_f32 v172, v172, s20, v13
	v_med3_f32 v173, v173, s20, v13
	v_med3_f32 v174, v174, s20, v13
	v_med3_f32 v175, v175, s20, v13
	v_med3_f32 v176, v176, s20, v13
	v_med3_f32 v177, v177, s20, v13
	v_med3_f32 v196, v196, s20, v13
	v_med3_f32 v197, v197, s20, v13
	v_med3_f32 v198, v198, s20, v13
	v_med3_f32 v199, v199, s20, v13
	v_med3_f32 v200, v200, s20, v13
	v_med3_f32 v201, v201, s20, v13
	v_med3_f32 v202, v202, s20, v13
	v_med3_f32 v203, v203, s20, v13
	v_mov_b32_e32 v208, 0
	v_mov_b32_e32 v209, 0
	v_mov_b32_e32 v210, 0
	v_mov_b32_e32 v211, 0
	v_cvt_pk_fp8_f32 v208, v170, v171
	v_cvt_pk_fp8_f32 v209, v174, v175
	v_cvt_pk_fp8_f32 v210, v196, v197
	v_cvt_pk_fp8_f32 v211, v200, v201
	v_cvt_pk_fp8_f32 v208, v172, v173 op_sel:[0,0,1]
	v_cvt_pk_fp8_f32 v209, v176, v177 op_sel:[0,0,1]
	v_cvt_pk_fp8_f32 v210, v198, v199 op_sel:[0,0,1]
	v_cvt_pk_fp8_f32 v211, v202, v203 op_sel:[0,0,1]
	s_nop 0
	global_store_dwordx4 v11, v[208:211], s[14:15]
	ds_read_b32 v170, v9
	ds_read_b32 v171, v9 offset:512
	ds_read_b32 v172, v9 offset:1024
	ds_read_b32 v173, v9 offset:1536
	ds_read_b32 v174, v9 offset:2048
	ds_read_b32 v175, v9 offset:2560
	ds_read_b32 v176, v9 offset:3072
	ds_read_b32 v177, v9 offset:3584
	ds_read_b32 v196, v9 offset:4096
	ds_read_b32 v197, v9 offset:4608
	ds_read_b32 v198, v9 offset:5120
	ds_read_b32 v199, v9 offset:5632
	ds_read_b32 v200, v9 offset:6144
	ds_read_b32 v201, v9 offset:6656
	ds_read_b32 v202, v9 offset:7168
	ds_read_b32 v203, v9 offset:7680
	s_waitcnt lgkmcnt(0)
	v_max_f32_e32 v170, v170, v170
	v_max_f32_e32 v171, v171, v171
	v_max_f32_e32 v172, v172, v172
	v_max_f32_e32 v173, v173, v173
	v_max_f32_e32 v174, v174, v174
	v_max_f32_e32 v175, v175, v175
	v_max_f32_e32 v176, v176, v176
	v_max_f32_e32 v177, v177, v177
	v_max_f32_e32 v196, v196, v196
	v_max_f32_e32 v197, v197, v197
	v_max_f32_e32 v198, v198, v198
	v_max_f32_e32 v199, v199, v199
	v_max_f32_e32 v200, v200, v200
	v_max_f32_e32 v201, v201, v201
	v_max_f32_e32 v202, v202, v202
	v_max_f32_e32 v203, v203, v203
	v_med3_f32 v170, v170, s20, v13
	v_med3_f32 v171, v171, s20, v13
	v_med3_f32 v172, v172, s20, v13
	v_med3_f32 v173, v173, s20, v13
	v_med3_f32 v174, v174, s20, v13
	v_med3_f32 v175, v175, s20, v13
	v_med3_f32 v176, v176, s20, v13
	v_med3_f32 v177, v177, s20, v13
	v_med3_f32 v196, v196, s20, v13
	v_med3_f32 v197, v197, s20, v13
	v_med3_f32 v198, v198, s20, v13
	v_med3_f32 v199, v199, s20, v13
	v_med3_f32 v200, v200, s20, v13
	v_med3_f32 v201, v201, s20, v13
	v_med3_f32 v202, v202, s20, v13
	v_med3_f32 v203, v203, s20, v13
	v_mov_b32_e32 v208, 0
	v_mov_b32_e32 v209, 0
	v_mov_b32_e32 v210, 0
	v_mov_b32_e32 v211, 0
	v_cvt_pk_fp8_f32 v208, v170, v171
	v_cvt_pk_fp8_f32 v209, v174, v175
	v_cvt_pk_fp8_f32 v210, v196, v197
	v_cvt_pk_fp8_f32 v211, v200, v201
	v_cvt_pk_fp8_f32 v208, v172, v173 op_sel:[0,0,1]
	v_cvt_pk_fp8_f32 v209, v176, v177 op_sel:[0,0,1]
	v_cvt_pk_fp8_f32 v210, v198, v199 op_sel:[0,0,1]
	v_cvt_pk_fp8_f32 v211, v202, v203 op_sel:[0,0,1]
	s_nop 0
	global_store_dwordx4 v12, v[208:211], s[14:15]
	s_waitcnt vmcnt(28)
	v_mul_f32_e32 v100, 0x43000000, v100
	v_mul_f32_e32 v101, 0x43000000, v101
	v_mul_f32_e32 v102, 0x43000000, v102
	v_mul_f32_e32 v103, 0x43000000, v103
	ds_write_b128 v4, v[100:103]
	v_mul_f32_e32 v104, 0x43000000, v104
	v_mul_f32_e32 v105, 0x43000000, v105
	v_mul_f32_e32 v106, 0x43000000, v106
	v_mul_f32_e32 v107, 0x43000000, v107
	ds_write_b128 v4, v[104:107] offset:1024
	v_mul_f32_e32 v108, 0x43000000, v108
	v_mul_f32_e32 v109, 0x43000000, v109
	v_mul_f32_e32 v110, 0x43000000, v110
	v_mul_f32_e32 v111, 0x43000000, v111
	ds_write_b128 v4, v[108:111] offset:2048
	v_mul_f32_e32 v112, 0x43000000, v112
	v_mul_f32_e32 v113, 0x43000000, v113
	v_mul_f32_e32 v114, 0x43000000, v114
	v_mul_f32_e32 v115, 0x43000000, v115
	ds_write_b128 v4, v[112:115] offset:3072
	v_mul_f32_e32 v116, 0x43000000, v116
	v_mul_f32_e32 v117, 0x43000000, v117
	v_mul_f32_e32 v118, 0x43000000, v118
	v_mul_f32_e32 v119, 0x43000000, v119
	ds_write_b128 v4, v[116:119] offset:4096
	v_mul_f32_e32 v120, 0x43000000, v120
	v_mul_f32_e32 v121, 0x43000000, v121
	v_mul_f32_e32 v122, 0x43000000, v122
	v_mul_f32_e32 v123, 0x43000000, v123
	ds_write_b128 v4, v[120:123] offset:5120
	v_mul_f32_e32 v124, 0x43000000, v124
	v_mul_f32_e32 v125, 0x43000000, v125
	v_mul_f32_e32 v126, 0x43000000, v126
	v_mul_f32_e32 v127, 0x43000000, v127
	ds_write_b128 v4, v[124:127] offset:6144
	v_mul_f32_e32 v128, 0x43000000, v128
	v_mul_f32_e32 v129, 0x43000000, v129
	v_mul_f32_e32 v130, 0x43000000, v130
	v_mul_f32_e32 v131, 0x43000000, v131
	ds_write_b128 v4, v[128:131] offset:7168
	s_waitcnt lgkmcnt(0)
	s_barrier
; #define GAS __attribute__((address_space(1)))
; #define LAS __attribute__((address_space(3)))
; #define LDS_WAIT() asm volatile("s_waitcnt lgkmcnt(0)" ::: "memory")
;     ...
;     for (int i = 0; i < 32; ++i) v[i] = sc >= 0 ? W[(size_t)(k0 + 2 * i + (lane >> 5)) * Nsrc + sc] : 0.f;
; #pragma unroll
;     for (int i = 0; i < 32; ++i) { const int k = k0 + 2 * i + (lane >> 5); float x = v[i] * wscale; if (KS) x *= (k < ksplit ? ksA[k] : ksB[k - ksplit]); scr[(2 * i + (lane >> 5)) * 33 + (lane & 31)] = x; }
;     LDS_WAIT(); asm volatile("" ::: "memory");
;     const int c = lane & 7;
; #pragma unroll
;     for (int j = 0; j < 4; ++j) { const int n = (lane >> 3) + 8 * j; const LAS float* s = scr + (8 * c) * 33 + n;
;         const unsigned long long o = (unsigned long long)pg8::pk4_fp8(s[0 * 33], s[1 * 33], s[2 * 33], s[3 * 33]) | ((unsigned long long)pg8::pk4_fp8(s[4 * 33], s[5 * 33], s[6 * 33], s[7 * 33]) << 32);
;         *(GAS unsigned long long*)(WT + (size_t)(n0 + n) * K + k0 + 8 * c) = o; }
	s_add_i32 s17, s16, 576
	s_min_u32 s17, s17, 0xfff
	s_lshr_b32 s18, s17, 5
	s_add_i32 s18, s18, 0
	s_and_b32 s19, s17, 31
	s_lshl_b32 s18, s18, 21
	s_lshl_b32 s19, s19, 9
	s_add_u32 s18, s18, s19
	s_add_u32 s12, s2, s18
	s_addc_u32 s13, s3, 0
	global_load_dwordx4 v[100:103], v10, s[12:13]
	s_add_u32 s12, s12, 0x8000
	s_addc_u32 s13, s13, 0
	global_load_dwordx4 v[104:107], v10, s[12:13]
	s_add_u32 s12, s12, 0x8000
	s_addc_u32 s13, s13, 0
	global_load_dwordx4 v[108:111], v10, s[12:13]
	s_add_u32 s12, s12, 0x8000
	s_addc_u32 s13, s13, 0
	global_load_dwordx4 v[112:115], v10, s[12:13]
	s_add_u32 s12, s12, 0x8000
	s_addc_u32 s13, s13, 0
	global_load_dwordx4 v[116:119], v10, s[12:13]
	s_add_u32 s12, s12, 0x8000
	s_addc_u32 s13, s13, 0
	global_load_dwordx4 v[120:123], v10, s[12:13]
	s_add_u32 s12, s12, 0x8000
	s_addc_u32 s13, s13, 0
	global_load_dwordx4 v[124:127], v10, s[12:13]
	s_add_u32 s12, s12, 0x8000
	s_addc_u32 s13, s13, 0
	global_load_dwordx4 v[128:131], v10, s[12:13]
	s_add_i32 s17, s16, 192
	s_min_u32 s17, s17, 0xfff
	s_lshr_b32 s18, s17, 5
	s_add_i32 s18, s18, 0
	s_and_b32 s19, s17, 31
	s_lshl_b32 s19, s19, 21
	s_lshl_b32 s18, s18, 7
	s_add_u32 s18, s18, s19
	s_add_u32 s14, s4, s18
	s_addc_u32 s15, s5, 0
	ds_read_b32 v170, v6
	ds_read_b32 v171, v6 offset:512
	ds_read_b32 v172, v6 offset:1024
	ds_read_b32 v173, v6 offset:1536
	ds_read_b32 v174, v6 offset:2048
	ds_read_b32 v175, v6 offset:2560
	ds_read_b32 v176, v6 offset:3072
	ds_read_b32 v177, v6 offset:3584
	ds_read_b32 v196, v6 offset:4096
	ds_read_b32 v197, v6 offset:4608
	ds_read_b32 v198, v6 offset:5120
	ds_read_b32 v199, v6 offset:5632
	ds_read_b32 v200, v6 offset:6144
	ds_read_b32 v201, v6 offset:6656
	ds_read_b32 v202, v6 offset:7168
	ds_read_b32 v203, v6 offset:7680
	s_waitcnt lgkmcnt(0)
	v_max_f32_e32 v170, v170, v170
	v_max_f32_e32 v171, v171, v171
	v_max_f32_e32 v172, v172, v172
	v_max_f32_e32 v173, v173, v173
	v_max_f32_e32 v174, v174, v174
	v_max_f32_e32 v175, v175, v175
	v_max_f32_e32 v176, v176, v176
	v_max_f32_e32 v177, v177, v177
	v_max_f32_e32 v196, v196, v196
	v_max_f32_e32 v197, v197, v197
	v_max_f32_e32 v198, v198, v198
	v_max_f32_e32 v199, v199, v199
	v_max_f32_e32 v200, v200, v200
	v_max_f32_e32 v201, v201, v201
	v_max_f32_e32 v202, v202, v202
	v_max_f32_e32 v203, v203, v203
	v_med3_f32 v170, v170, s20, v13
	v_med3_f32 v171, v171, s20, v13
	v_med3_f32 v172, v172, s20, v13
	v_med3_f32 v173, v173, s20, v13
	v_med3_f32 v174, v174, s20, v13
	v_med3_f32 v175, v175, s20, v13
	v_med3_f32 v176, v176, s20, v13
	v_med3_f32 v177, v177, s20, v13
	v_med3_f32 v196, v196, s20, v13
	v_med3_f32 v197, v197, s20, v13
	v_med3_f32 v198, v198, s20, v13
	v_med3_f32 v199, v199, s20, v13
	v_med3_f32 v200, v200, s20, v13
	v_med3_f32 v201, v201, s20, v13
	v_med3_f32 v202, v202, s20, v13
	v_med3_f32 v203, v203, s20, v13
	v_mov_b32_e32 v208, 0
	v_mov_b32_e32 v209, 0
	v_mov_b32_e32 v210, 0
	v_mov_b32_e32 v211, 0
	v_cvt_pk_fp8_f32 v208, v170, v171
	v_cvt_pk_fp8_f32 v209, v174, v175
	v_cvt_pk_fp8_f32 v210, v196, v197
	v_cvt_pk_fp8_f32 v211, v200, v201
	v_cvt_pk_fp8_f32 v208, v172, v173 op_sel:[0,0,1]
	v_cvt_pk_fp8_f32 v209, v176, v177 op_sel:[0,0,1]
	v_cvt_pk_fp8_f32 v210, v198, v199 op_sel:[0,0,1]
	v_cvt_pk_fp8_f32 v211, v202, v203 op_sel:[0,0,1]
	s_nop 0
	global_store_dwordx4 v11, v[208:211], s[14:15]
	ds_read_b32 v170, v8
	ds_read_b32 v171, v8 offset:512
	ds_read_b32 v172, v8 offset:1024
	ds_read_b32 v173, v8 offset:1536
	ds_read_b32 v174, v8 offset:2048
	ds_read_b32 v175, v8 offset:2560
	ds_read_b32 v176, v8 offset:3072
	ds_read_b32 v177, v8 offset:3584
	ds_read_b32 v196, v8 offset:4096
	ds_read_b32 v197, v8 offset:4608
	ds_read_b32 v198, v8 offset:5120
	ds_read_b32 v199, v8 offset:5632
	ds_read_b32 v200, v8 offset:6144
	ds_read_b32 v201, v8 offset:6656
	ds_read_b32 v202, v8 offset:7168
	ds_read_b32 v203, v8 offset:7680
	s_waitcnt lgkmcnt(0)
	v_max_f32_e32 v170, v170, v170
	v_max_f32_e32 v171, v171, v171
	v_max_f32_e32 v172, v172, v172
	v_max_f32_e32 v173, v173, v173
	v_max_f32_e32 v174, v174, v174
	v_max_f32_e32 v175, v175, v175
	v_max_f32_e32 v176, v176, v176
	v_max_f32_e32 v177, v177, v177
	v_max_f32_e32 v196, v196, v196
	v_max_f32_e32 v197, v197, v197
	v_max_f32_e32 v198, v198, v198
	v_max_f32_e32 v199, v199, v199
	v_max_f32_e32 v200, v200, v200
	v_max_f32_e32 v201, v201, v201
	v_max_f32_e32 v202, v202, v202
	v_max_f32_e32 v203, v203, v203
	v_med3_f32 v170, v170, s20, v13
	v_med3_f32 v171, v171, s20, v13
	v_med3_f32 v172, v172, s20, v13
	v_med3_f32 v173, v173, s20, v13
	v_med3_f32 v174, v174, s20, v13
	v_med3_f32 v175, v175, s20, v13
	v_med3_f32 v176, v176, s20, v13
	v_med3_f32 v177, v177, s20, v13
	v_med3_f32 v196, v196, s20, v13
	v_med3_f32 v197, v197, s20, v13
	v_med3_f32 v198, v198, s20, v13
	v_med3_f32 v199, v199, s20, v13
	v_med3_f32 v200, v200, s20, v13
	v_med3_f32 v201, v201, s20, v13
	v_med3_f32 v202, v202, s20, v13
	v_med3_f32 v203, v203, s20, v13
	v_mov_b32_e32 v208, 0
	v_mov_b32_e32 v209, 0
	v_mov_b32_e32 v210, 0
	v_mov_b32_e32 v211, 0
	v_cvt_pk_fp8_f32 v208, v170, v171
	v_cvt_pk_fp8_f32 v209, v174, v175
	v_cvt_pk_fp8_f32 v210, v196, v197
	v_cvt_pk_fp8_f32 v211, v200, v201
	v_cvt_pk_fp8_f32 v208, v172, v173 op_sel:[0,0,1]
	v_cvt_pk_fp8_f32 v209, v176, v177 op_sel:[0,0,1]
	v_cvt_pk_fp8_f32 v210, v198, v199 op_sel:[0,0,1]
	v_cvt_pk_fp8_f32 v211, v202, v203 op_sel:[0,0,1]
	s_nop 0
	global_store_dwordx4 v12, v[208:211], s[14:15]
	s_waitcnt vmcnt(30)
	v_mul_f32_e32 v132, 0x43000000, v132
	v_mul_f32_e32 v133, 0x43000000, v133
	v_mul_f32_e32 v134, 0x43000000, v134
	v_mul_f32_e32 v135, 0x43000000, v135
	ds_write_b128 v5, v[132:135]
	v_mul_f32_e32 v136, 0x43000000, v136
	v_mul_f32_e32 v137, 0x43000000, v137
	v_mul_f32_e32 v138, 0x43000000, v138
	v_mul_f32_e32 v139, 0x43000000, v139
	ds_write_b128 v5, v[136:139] offset:1024
	v_mul_f32_e32 v140, 0x43000000, v140
	v_mul_f32_e32 v141, 0x43000000, v141
	v_mul_f32_e32 v142, 0x43000000, v142
	v_mul_f32_e32 v143, 0x43000000, v143
	ds_write_b128 v5, v[140:143] offset:2048
	v_mul_f32_e32 v144, 0x43000000, v144
	v_mul_f32_e32 v145, 0x43000000, v145
	v_mul_f32_e32 v146, 0x43000000, v146
	v_mul_f32_e32 v147, 0x43000000, v147
	ds_write_b128 v5, v[144:147] offset:3072
	v_mul_f32_e32 v148, 0x43000000, v148
	v_mul_f32_e32 v149, 0x43000000, v149
	v_mul_f32_e32 v150, 0x43000000, v150
	v_mul_f32_e32 v151, 0x43000000, v151
	ds_write_b128 v5, v[148:151] offset:4096
	v_mul_f32_e32 v152, 0x43000000, v152
	v_mul_f32_e32 v153, 0x43000000, v153
	v_mul_f32_e32 v154, 0x43000000, v154
	v_mul_f32_e32 v155, 0x43000000, v155
	ds_write_b128 v5, v[152:155] offset:5120
	v_mul_f32_e32 v156, 0x43000000, v156
	v_mul_f32_e32 v157, 0x43000000, v157
	v_mul_f32_e32 v158, 0x43000000, v158
	v_mul_f32_e32 v159, 0x43000000, v159
	ds_write_b128 v5, v[156:159] offset:6144
	v_mul_f32_e32 v160, 0x43000000, v160
	v_mul_f32_e32 v161, 0x43000000, v161
	v_mul_f32_e32 v162, 0x43000000, v162
	v_mul_f32_e32 v163, 0x43000000, v163
	ds_write_b128 v5, v[160:163] offset:7168
	s_waitcnt lgkmcnt(0)
	s_barrier
; #define GAS __attribute__((address_space(1)))
; #define LAS __attribute__((address_space(3)))
; #define LDS_WAIT() asm volatile("s_waitcnt lgkmcnt(0)" ::: "memory")
;     ...
;     for (int i = 0; i < 32; ++i) v[i] = sc >= 0 ? W[(size_t)(k0 + 2 * i + (lane >> 5)) * Nsrc + sc] : 0.f;
; #pragma unroll
;     for (int i = 0; i < 32; ++i) { const int k = k0 + 2 * i + (lane >> 5); float x = v[i] * wscale; if (KS) x *= (k < ksplit ? ksA[k] : ksB[k - ksplit]); scr[(2 * i + (lane >> 5)) * 33 + (lane & 31)] = x; }
;     LDS_WAIT(); asm volatile("" ::: "memory");
;     const int c = lane & 7;
; #pragma unroll
;     for (int j = 0; j < 4; ++j) { const int n = (lane >> 3) + 8 * j; const LAS float* s = scr + (8 * c) * 33 + n;
;         const unsigned long long o = (unsigned long long)pg8::pk4_fp8(s[0 * 33], s[1 * 33], s[2 * 33], s[3 * 33]) | ((unsigned long long)pg8::pk4_fp8(s[4 * 33], s[5 * 33], s[6 * 33], s[7 * 33]) << 32);
;         *(GAS unsigned long long*)(WT + (size_t)(n0 + n) * K + k0 + 8 * c) = o; }
	s_add_i32 s17, s16, 672
	s_min_u32 s17, s17, 0xfff
	s_lshr_b32 s18, s17, 5
	s_add_i32 s18, s18, 0
	s_and_b32 s19, s17, 31
	s_lshl_b32 s18, s18, 21
	s_lshl_b32 s19, s19, 9
	s_add_u32 s18, s18, s19
	s_add_u32 s12, s2, s18
	s_addc_u32 s13, s3, 0
	global_load_dwordx4 v[132:135], v10, s[12:13]
	s_add_u32 s12, s12, 0x8000
	s_addc_u32 s13, s13, 0
	global_load_dwordx4 v[136:139], v10, s[12:13]
	s_add_u32 s12, s12, 0x8000
	s_addc_u32 s13, s13, 0
	global_load_dwordx4 v[140:143], v10, s[12:13]
	s_add_u32 s12, s12, 0x8000
	s_addc_u32 s13, s13, 0
	global_load_dwordx4 v[144:147], v10, s[12:13]
	s_add_u32 s12, s12, 0x8000
	s_addc_u32 s13, s13, 0
	global_load_dwordx4 v[148:151], v10, s[12:13]
	s_add_u32 s12, s12, 0x8000
	s_addc_u32 s13, s13, 0
	global_load_dwordx4 v[152:155], v10, s[12:13]
	s_add_u32 s12, s12, 0x8000
	s_addc_u32 s13, s13, 0
	global_load_dwordx4 v[156:159], v10, s[12:13]
	s_add_u32 s12, s12, 0x8000
	s_addc_u32 s13, s13, 0
	global_load_dwordx4 v[160:163], v10, s[12:13]
	s_add_i32 s17, s16, 288
	s_min_u32 s17, s17, 0xfff
	s_lshr_b32 s18, s17, 5
	s_add_i32 s18, s18, 0
	s_and_b32 s19, s17, 31
	s_lshl_b32 s19, s19, 21
	s_lshl_b32 s18, s18, 7
	s_add_u32 s18, s18, s19
	s_add_u32 s14, s4, s18
	s_addc_u32 s15, s5, 0
	ds_read_b32 v170, v7
	ds_read_b32 v171, v7 offset:512
	ds_read_b32 v172, v7 offset:1024
	ds_read_b32 v173, v7 offset:1536
	ds_read_b32 v174, v7 offset:2048
	ds_read_b32 v175, v7 offset:2560
	ds_read_b32 v176, v7 offset:3072
	ds_read_b32 v177, v7 offset:3584
	ds_read_b32 v196, v7 offset:4096
	ds_read_b32 v197, v7 offset:4608
	ds_read_b32 v198, v7 offset:5120
	ds_read_b32 v199, v7 offset:5632
	ds_read_b32 v200, v7 offset:6144
	ds_read_b32 v201, v7 offset:6656
	ds_read_b32 v202, v7 offset:7168
	ds_read_b32 v203, v7 offset:7680
	s_waitcnt lgkmcnt(0)
	v_max_f32_e32 v170, v170, v170
	v_max_f32_e32 v171, v171, v171
	v_max_f32_e32 v172, v172, v172
	v_max_f32_e32 v173, v173, v173
	v_max_f32_e32 v174, v174, v174
	v_max_f32_e32 v175, v175, v175
	v_max_f32_e32 v176, v176, v176
	v_max_f32_e32 v177, v177, v177
	v_max_f32_e32 v196, v196, v196
	v_max_f32_e32 v197, v197, v197
	v_max_f32_e32 v198, v198, v198
	v_max_f32_e32 v199, v199, v199
	v_max_f32_e32 v200, v200, v200
	v_max_f32_e32 v201, v201, v201
	v_max_f32_e32 v202, v202, v202
	v_max_f32_e32 v203, v203, v203
	v_med3_f32 v170, v170, s20, v13
	v_med3_f32 v171, v171, s20, v13
	v_med3_f32 v172, v172, s20, v13
	v_med3_f32 v173, v173, s20, v13
	v_med3_f32 v174, v174, s20, v13
	v_med3_f32 v175, v175, s20, v13
	v_med3_f32 v176, v176, s20, v13
	v_med3_f32 v177, v177, s20, v13
	v_med3_f32 v196, v196, s20, v13
	v_med3_f32 v197, v197, s20, v13
	v_med3_f32 v198, v198, s20, v13
	v_med3_f32 v199, v199, s20, v13
	v_med3_f32 v200, v200, s20, v13
	v_med3_f32 v201, v201, s20, v13
	v_med3_f32 v202, v202, s20, v13
	v_med3_f32 v203, v203, s20, v13
	v_mov_b32_e32 v208, 0
	v_mov_b32_e32 v209, 0
	v_mov_b32_e32 v210, 0
	v_mov_b32_e32 v211, 0
	v_cvt_pk_fp8_f32 v208, v170, v171
	v_cvt_pk_fp8_f32 v209, v174, v175
	v_cvt_pk_fp8_f32 v210, v196, v197
	v_cvt_pk_fp8_f32 v211, v200, v201
	v_cvt_pk_fp8_f32 v208, v172, v173 op_sel:[0,0,1]
	v_cvt_pk_fp8_f32 v209, v176, v177 op_sel:[0,0,1]
	v_cvt_pk_fp8_f32 v210, v198, v199 op_sel:[0,0,1]
	v_cvt_pk_fp8_f32 v211, v202, v203 op_sel:[0,0,1]
	s_nop 0
	global_store_dwordx4 v11, v[208:211], s[14:15]
	ds_read_b32 v170, v9
	ds_read_b32 v171, v9 offset:512
	ds_read_b32 v172, v9 offset:1024
	ds_read_b32 v173, v9 offset:1536
	ds_read_b32 v174, v9 offset:2048
	ds_read_b32 v175, v9 offset:2560
	ds_read_b32 v176, v9 offset:3072
	ds_read_b32 v177, v9 offset:3584
	ds_read_b32 v196, v9 offset:4096
	ds_read_b32 v197, v9 offset:4608
	ds_read_b32 v198, v9 offset:5120
	ds_read_b32 v199, v9 offset:5632
	ds_read_b32 v200, v9 offset:6144
	ds_read_b32 v201, v9 offset:6656
	ds_read_b32 v202, v9 offset:7168
	ds_read_b32 v203, v9 offset:7680
	s_waitcnt lgkmcnt(0)
	v_max_f32_e32 v170, v170, v170
	v_max_f32_e32 v171, v171, v171
	v_max_f32_e32 v172, v172, v172
	v_max_f32_e32 v173, v173, v173
	v_max_f32_e32 v174, v174, v174
	v_max_f32_e32 v175, v175, v175
	v_max_f32_e32 v176, v176, v176
	v_max_f32_e32 v177, v177, v177
	v_max_f32_e32 v196, v196, v196
	v_max_f32_e32 v197, v197, v197
	v_max_f32_e32 v198, v198, v198
	v_max_f32_e32 v199, v199, v199
	v_max_f32_e32 v200, v200, v200
	v_max_f32_e32 v201, v201, v201
	v_max_f32_e32 v202, v202, v202
	v_max_f32_e32 v203, v203, v203
	v_med3_f32 v170, v170, s20, v13
	v_med3_f32 v171, v171, s20, v13
	v_med3_f32 v172, v172, s20, v13
	v_med3_f32 v173, v173, s20, v13
	v_med3_f32 v174, v174, s20, v13
	v_med3_f32 v175, v175, s20, v13
	v_med3_f32 v176, v176, s20, v13
	v_med3_f32 v177, v177, s20, v13
	v_med3_f32 v196, v196, s20, v13
	v_med3_f32 v197, v197, s20, v13
	v_med3_f32 v198, v198, s20, v13
	v_med3_f32 v199, v199, s20, v13
	v_med3_f32 v200, v200, s20, v13
	v_med3_f32 v201, v201, s20, v13
	v_med3_f32 v202, v202, s20, v13
	v_med3_f32 v203, v203, s20, v13
	v_mov_b32_e32 v208, 0
	v_mov_b32_e32 v209, 0
	v_mov_b32_e32 v210, 0
	v_mov_b32_e32 v211, 0
	v_cvt_pk_fp8_f32 v208, v170, v171
	v_cvt_pk_fp8_f32 v209, v174, v175
	v_cvt_pk_fp8_f32 v210, v196, v197
	v_cvt_pk_fp8_f32 v211, v200, v201
	v_cvt_pk_fp8_f32 v208, v172, v173 op_sel:[0,0,1]
	v_cvt_pk_fp8_f32 v209, v176, v177 op_sel:[0,0,1]
	v_cvt_pk_fp8_f32 v210, v198, v199 op_sel:[0,0,1]
	v_cvt_pk_fp8_f32 v211, v202, v203 op_sel:[0,0,1]
	s_nop 0
	global_store_dwordx4 v12, v[208:211], s[14:15]
	s_waitcnt vmcnt(32)
	v_mul_f32_e32 v36, 0x43000000, v36
	v_mul_f32_e32 v37, 0x43000000, v37
	v_mul_f32_e32 v38, 0x43000000, v38
	v_mul_f32_e32 v39, 0x43000000, v39
	ds_write_b128 v4, v[36:39]
	v_mul_f32_e32 v40, 0x43000000, v40
	v_mul_f32_e32 v41, 0x43000000, v41
	v_mul_f32_e32 v42, 0x43000000, v42
	v_mul_f32_e32 v43, 0x43000000, v43
	ds_write_b128 v4, v[40:43] offset:1024
	v_mul_f32_e32 v44, 0x43000000, v44
	v_mul_f32_e32 v45, 0x43000000, v45
	v_mul_f32_e32 v46, 0x43000000, v46
	v_mul_f32_e32 v47, 0x43000000, v47
	ds_write_b128 v4, v[44:47] offset:2048
	v_mul_f32_e32 v48, 0x43000000, v48
	v_mul_f32_e32 v49, 0x43000000, v49
	v_mul_f32_e32 v50, 0x43000000, v50
	v_mul_f32_e32 v51, 0x43000000, v51
	ds_write_b128 v4, v[48:51] offset:3072
	v_mul_f32_e32 v52, 0x43000000, v52
	v_mul_f32_e32 v53, 0x43000000, v53
	v_mul_f32_e32 v54, 0x43000000, v54
	v_mul_f32_e32 v55, 0x43000000, v55
	ds_write_b128 v4, v[52:55] offset:4096
	v_mul_f32_e32 v56, 0x43000000, v56
	v_mul_f32_e32 v57, 0x43000000, v57
	v_mul_f32_e32 v58, 0x43000000, v58
	v_mul_f32_e32 v59, 0x43000000, v59
	ds_write_b128 v4, v[56:59] offset:5120
	v_mul_f32_e32 v60, 0x43000000, v60
	v_mul_f32_e32 v61, 0x43000000, v61
	v_mul_f32_e32 v62, 0x43000000, v62
	v_mul_f32_e32 v63, 0x43000000, v63
	ds_write_b128 v4, v[60:63] offset:6144
	v_mul_f32_e32 v64, 0x43000000, v64
	v_mul_f32_e32 v65, 0x43000000, v65
	v_mul_f32_e32 v66, 0x43000000, v66
	v_mul_f32_e32 v67, 0x43000000, v67
	ds_write_b128 v4, v[64:67] offset:7168
	s_waitcnt lgkmcnt(0)
	s_barrier
; #define GAS __attribute__((address_space(1)))
; #define LAS __attribute__((address_space(3)))
; #define LDS_WAIT() asm volatile("s_waitcnt lgkmcnt(0)" ::: "memory")
; __device__ __forceinline__ unsigned pk4_fp8(float a, float b, float c, float d) {
;     a = fminf(fmaxf(a, -448.f), 448.f); b = fminf(fmaxf(b, -448.f), 448.f); c = fminf(fmaxf(c, -448.f), 448.f); d = fminf(fmaxf(d, -448.f), 448.f);
;     int w = __builtin_amdgcn_cvt_pk_fp8_f32(a, b, 0, false); w = __builtin_amdgcn_cvt_pk_fp8_f32(c, d, w, true); return (unsigned)w; }
;     const int pr = item >> 1, kb = 2 * (pr / nblk) + (item & 1), nb = pr % nblk, k0 = 64 * kb, n0 = 32 * nb;
;     const int nr = n0 + (lane & 31); const int sc = MAP == 1 ? src_col_in(nr) : nr;
;     float v[32];
; #pragma unroll
;     for (int i = 0; i < 32; ++i) v[i] = sc >= 0 ? W[(size_t)(k0 + 2 * i + (lane >> 5)) * Nsrc + sc] : 0.f;
; #pragma unroll
;     for (int i = 0; i < 32; ++i) { const int k = k0 + 2 * i + (lane >> 5); float x = v[i] * wscale; if (KS) x *= (k < ksplit ? ksA[k] : ksB[k - ksplit]); scr[(2 * i + (lane >> 5)) * 33 + (lane & 31)] = x; }
;     LDS_WAIT(); asm volatile("" ::: "memory");
;     const int c = lane & 7;
; #pragma unroll
;     for (int j = 0; j < 4; ++j) { const int n = (lane >> 3) + 8 * j; const LAS float* s = scr + (8 * c) * 33 + n;
;         const unsigned long long o = (unsigned long long)pg8::pk4_fp8(s[0 * 33], s[1 * 33], s[2 * 33], s[3 * 33]) | ((unsigned long long)pg8::pk4_fp8(s[4 * 33], s[5 * 33], s[6 * 33], s[7 * 33]) << 32);
;         *(GAS unsigned long long*)(WT + (size_t)(n0 + n) * K + k0 + 8 * c) = o; }
;     LDS_WAIT(); asm volatile("" ::: "memory");
; }
	s_add_i32 s17, s16, 768
	s_min_u32 s17, s17, 0xfff
	s_lshr_b32 s18, s17, 5
	s_add_i32 s18, s18, 0
	s_and_b32 s19, s17, 31
	s_lshl_b32 s18, s18, 21
	s_lshl_b32 s19, s19, 9
	s_add_u32 s18, s18, s19
	s_add_u32 s12, s2, s18
	s_addc_u32 s13, s3, 0
	global_load_dwordx4 v[36:39], v10, s[12:13]
	s_add_u32 s12, s12, 0x8000
	s_addc_u32 s13, s13, 0
	global_load_dwordx4 v[40:43], v10, s[12:13]
	s_add_u32 s12, s12, 0x8000
	s_addc_u32 s13, s13, 0
	global_load_dwordx4 v[44:47], v10, s[12:13]
	s_add_u32 s12, s12, 0x8000
	s_addc_u32 s13, s13, 0
	global_load_dwordx4 v[48:51], v10, s[12:13]
	s_add_u32 s12, s12, 0x8000
	s_addc_u32 s13, s13, 0
	global_load_dwordx4 v[52:55], v10, s[12:13]
	s_add_u32 s12, s12, 0x8000
	s_addc_u32 s13, s13, 0
	global_load_dwordx4 v[56:59], v10, s[12:13]
	s_add_u32 s12, s12, 0x8000
	s_addc_u32 s13, s13, 0
	global_load_dwordx4 v[60:63], v10, s[12:13]
	s_add_u32 s12, s12, 0x8000
	s_addc_u32 s13, s13, 0
	global_load_dwordx4 v[64:67], v10, s[12:13]
	s_add_i32 s17, s16, 384
	s_min_u32 s17, s17, 0xfff
	s_lshr_b32 s18, s17, 5
	s_add_i32 s18, s18, 0
	s_and_b32 s19, s17, 31
	s_lshl_b32 s19, s19, 21
	s_lshl_b32 s18, s18, 7
	s_add_u32 s18, s18, s19
	s_add_u32 s14, s4, s18
	s_addc_u32 s15, s5, 0
	ds_read_b32 v170, v6
	ds_read_b32 v171, v6 offset:512
	ds_read_b32 v172, v6 offset:1024
	ds_read_b32 v173, v6 offset:1536
	ds_read_b32 v174, v6 offset:2048
	ds_read_b32 v175, v6 offset:2560
	ds_read_b32 v176, v6 offset:3072
	ds_read_b32 v177, v6 offset:3584
	ds_read_b32 v196, v6 offset:4096
	ds_read_b32 v197, v6 offset:4608
	ds_read_b32 v198, v6 offset:5120
	ds_read_b32 v199, v6 offset:5632
	ds_read_b32 v200, v6 offset:6144
	ds_read_b32 v201, v6 offset:6656
	ds_read_b32 v202, v6 offset:7168
	ds_read_b32 v203, v6 offset:7680
	s_waitcnt lgkmcnt(0)
	v_max_f32_e32 v170, v170, v170
	v_max_f32_e32 v171, v171, v171
	v_max_f32_e32 v172, v172, v172
	v_max_f32_e32 v173, v173, v173
	v_max_f32_e32 v174, v174, v174
	v_max_f32_e32 v175, v175, v175
	v_max_f32_e32 v176, v176, v176
	v_max_f32_e32 v177, v177, v177
	v_max_f32_e32 v196, v196, v196
	v_max_f32_e32 v197, v197, v197
	v_max_f32_e32 v198, v198, v198
	v_max_f32_e32 v199, v199, v199
	v_max_f32_e32 v200, v200, v200
	v_max_f32_e32 v201, v201, v201
	v_max_f32_e32 v202, v202, v202
	v_max_f32_e32 v203, v203, v203
	v_med3_f32 v170, v170, s20, v13
	v_med3_f32 v171, v171, s20, v13
	v_med3_f32 v172, v172, s20, v13
	v_med3_f32 v173, v173, s20, v13
	v_med3_f32 v174, v174, s20, v13
	v_med3_f32 v175, v175, s20, v13
	v_med3_f32 v176, v176, s20, v13
	v_med3_f32 v177, v177, s20, v13
	v_med3_f32 v196, v196, s20, v13
	v_med3_f32 v197, v197, s20, v13
	v_med3_f32 v198, v198, s20, v13
	v_med3_f32 v199, v199, s20, v13
	v_med3_f32 v200, v200, s20, v13
	v_med3_f32 v201, v201, s20, v13
	v_med3_f32 v202, v202, s20, v13
	v_med3_f32 v203, v203, s20, v13
	v_mov_b32_e32 v208, 0
	v_mov_b32_e32 v209, 0
	v_mov_b32_e32 v210, 0
	v_mov_b32_e32 v211, 0
	v_cvt_pk_fp8_f32 v208, v170, v171
	v_cvt_pk_fp8_f32 v209, v174, v175
	v_cvt_pk_fp8_f32 v210, v196, v197
	v_cvt_pk_fp8_f32 v211, v200, v201
	v_cvt_pk_fp8_f32 v208, v172, v173 op_sel:[0,0,1]
	v_cvt_pk_fp8_f32 v209, v176, v177 op_sel:[0,0,1]
	v_cvt_pk_fp8_f32 v210, v198, v199 op_sel:[0,0,1]
	v_cvt_pk_fp8_f32 v211, v202, v203 op_sel:[0,0,1]
	s_nop 0
	global_store_dwordx4 v11, v[208:211], s[14:15]
	ds_read_b32 v170, v8
	ds_read_b32 v171, v8 offset:512
	ds_read_b32 v172, v8 offset:1024
	ds_read_b32 v173, v8 offset:1536
	ds_read_b32 v174, v8 offset:2048
	ds_read_b32 v175, v8 offset:2560
	ds_read_b32 v176, v8 offset:3072
	ds_read_b32 v177, v8 offset:3584
	ds_read_b32 v196, v8 offset:4096
	ds_read_b32 v197, v8 offset:4608
	ds_read_b32 v198, v8 offset:5120
	ds_read_b32 v199, v8 offset:5632
	ds_read_b32 v200, v8 offset:6144
	ds_read_b32 v201, v8 offset:6656
	ds_read_b32 v202, v8 offset:7168
	ds_read_b32 v203, v8 offset:7680
	s_waitcnt lgkmcnt(0)
	v_max_f32_e32 v170, v170, v170
	v_max_f32_e32 v171, v171, v171
	v_max_f32_e32 v172, v172, v172
	v_max_f32_e32 v173, v173, v173
	v_max_f32_e32 v174, v174, v174
	v_max_f32_e32 v175, v175, v175
	v_max_f32_e32 v176, v176, v176
	v_max_f32_e32 v177, v177, v177
	v_max_f32_e32 v196, v196, v196
	v_max_f32_e32 v197, v197, v197
	v_max_f32_e32 v198, v198, v198
	v_max_f32_e32 v199, v199, v199
	v_max_f32_e32 v200, v200, v200
	v_max_f32_e32 v201, v201, v201
	v_max_f32_e32 v202, v202, v202
	v_max_f32_e32 v203, v203, v203
	v_med3_f32 v170, v170, s20, v13
	v_med3_f32 v171, v171, s20, v13
	v_med3_f32 v172, v172, s20, v13
	v_med3_f32 v173, v173, s20, v13
	v_med3_f32 v174, v174, s20, v13
	v_med3_f32 v175, v175, s20, v13
	v_med3_f32 v176, v176, s20, v13
	v_med3_f32 v177, v177, s20, v13
	v_med3_f32 v196, v196, s20, v13
	v_med3_f32 v197, v197, s20, v13
	v_med3_f32 v198, v198, s20, v13
	v_med3_f32 v199, v199, s20, v13
	v_med3_f32 v200, v200, s20, v13
	v_med3_f32 v201, v201, s20, v13
	v_med3_f32 v202, v202, s20, v13
	v_med3_f32 v203, v203, s20, v13
	v_mov_b32_e32 v208, 0
	v_mov_b32_e32 v209, 0
	v_mov_b32_e32 v210, 0
	v_mov_b32_e32 v211, 0
	v_cvt_pk_fp8_f32 v208, v170, v171
	v_cvt_pk_fp8_f32 v209, v174, v175
	v_cvt_pk_fp8_f32 v210, v196, v197
	v_cvt_pk_fp8_f32 v211, v200, v201
	v_cvt_pk_fp8_f32 v208, v172, v173 op_sel:[0,0,1]
	v_cvt_pk_fp8_f32 v209, v176, v177 op_sel:[0,0,1]
	v_cvt_pk_fp8_f32 v210, v198, v199 op_sel:[0,0,1]
	v_cvt_pk_fp8_f32 v211, v202, v203 op_sel:[0,0,1]
	s_nop 0
	global_store_dwordx4 v12, v[208:211], s[14:15]
	s_waitcnt vmcnt(32)
	v_mul_f32_e32 v68, 0x43000000, v68
	v_mul_f32_e32 v69, 0x43000000, v69
	v_mul_f32_e32 v70, 0x43000000, v70
	v_mul_f32_e32 v71, 0x43000000, v71
	ds_write_b128 v5, v[68:71]
	v_mul_f32_e32 v72, 0x43000000, v72
	v_mul_f32_e32 v73, 0x43000000, v73
	v_mul_f32_e32 v74, 0x43000000, v74
	v_mul_f32_e32 v75, 0x43000000, v75
	ds_write_b128 v5, v[72:75] offset:1024
	v_mul_f32_e32 v76, 0x43000000, v76
	v_mul_f32_e32 v77, 0x43000000, v77
	v_mul_f32_e32 v78, 0x43000000, v78
	v_mul_f32_e32 v79, 0x43000000, v79
	ds_write_b128 v5, v[76:79] offset:2048
	v_mul_f32_e32 v80, 0x43000000, v80
	v_mul_f32_e32 v81, 0x43000000, v81
	v_mul_f32_e32 v82, 0x43000000, v82
	v_mul_f32_e32 v83, 0x43000000, v83
	ds_write_b128 v5, v[80:83] offset:3072
	v_mul_f32_e32 v84, 0x43000000, v84
	v_mul_f32_e32 v85, 0x43000000, v85
	v_mul_f32_e32 v86, 0x43000000, v86
	v_mul_f32_e32 v87, 0x43000000, v87
	ds_write_b128 v5, v[84:87] offset:4096
	v_mul_f32_e32 v88, 0x43000000, v88
	v_mul_f32_e32 v89, 0x43000000, v89
	v_mul_f32_e32 v90, 0x43000000, v90
	v_mul_f32_e32 v91, 0x43000000, v91
	ds_write_b128 v5, v[88:91] offset:5120
	v_mul_f32_e32 v92, 0x43000000, v92
	v_mul_f32_e32 v93, 0x43000000, v93
	v_mul_f32_e32 v94, 0x43000000, v94
	v_mul_f32_e32 v95, 0x43000000, v95
	ds_write_b128 v5, v[92:95] offset:6144
	v_mul_f32_e32 v96, 0x43000000, v96
	v_mul_f32_e32 v97, 0x43000000, v97
	v_mul_f32_e32 v98, 0x43000000, v98
	v_mul_f32_e32 v99, 0x43000000, v99
	ds_write_b128 v5, v[96:99] offset:7168
	s_waitcnt lgkmcnt(0)
	s_barrier
; #define GAS __attribute__((address_space(1)))
; #define LAS __attribute__((address_space(3)))
; #define LDS_WAIT() asm volatile("s_waitcnt lgkmcnt(0)" ::: "memory")
; __device__ __forceinline__ unsigned pk4_fp8(float a, float b, float c, float d) {
;     a = fminf(fmaxf(a, -448.f), 448.f); b = fminf(fmaxf(b, -448.f), 448.f); c = fminf(fmaxf(c, -448.f), 448.f); d = fminf(fmaxf(d, -448.f), 448.f);
;     int w = __builtin_amdgcn_cvt_pk_fp8_f32(a, b, 0, false); w = __builtin_amdgcn_cvt_pk_fp8_f32(c, d, w, true); return (unsigned)w; }
;     const int pr = item >> 1, kb = 2 * (pr / nblk) + (item & 1), nb = pr % nblk, k0 = 64 * kb, n0 = 32 * nb;
;     const int nr = n0 + (lane & 31); const int sc = MAP == 1 ? src_col_in(nr) : nr;
;     float v[32];
; #pragma unroll
;     for (int i = 0; i < 32; ++i) v[i] = sc >= 0 ? W[(size_t)(k0 + 2 * i + (lane >> 5)) * Nsrc + sc] : 0.f;
; #pragma unroll
;     for (int i = 0; i < 32; ++i) { const int k = k0 + 2 * i + (lane >> 5); float x = v[i] * wscale; if (KS) x *= (k < ksplit ? ksA[k] : ksB[k - ksplit]); scr[(2 * i + (lane >> 5)) * 33 + (lane & 31)] = x; }
;     LDS_WAIT(); asm volatile("" ::: "memory");
;     const int c = lane & 7;
; #pragma unroll
;     for (int j = 0; j < 4; ++j) { const int n = (lane >> 3) + 8 * j; const LAS float* s = scr + (8 * c) * 33 + n;
;         const unsigned long long o = (unsigned long long)pg8::pk4_fp8(s[0 * 33], s[1 * 33], s[2 * 33], s[3 * 33]) | ((unsigned long long)pg8::pk4_fp8(s[4 * 33], s[5 * 33], s[6 * 33], s[7 * 33]) << 32);
;         *(GAS unsigned long long*)(WT + (size_t)(n0 + n) * K + k0 + 8 * c) = o; }
;     LDS_WAIT(); asm volatile("" ::: "memory");
; }
	s_add_i32 s17, s16, 864
	s_min_u32 s17, s17, 0xfff
	s_lshr_b32 s18, s17, 5
	s_add_i32 s18, s18, 0
	s_and_b32 s19, s17, 31
	s_lshl_b32 s18, s18, 21
	s_lshl_b32 s19, s19, 9
	s_add_u32 s18, s18, s19
	s_add_u32 s12, s2, s18
	s_addc_u32 s13, s3, 0
	global_load_dwordx4 v[68:71], v10, s[12:13]
	s_add_u32 s12, s12, 0x8000
	s_addc_u32 s13, s13, 0
	global_load_dwordx4 v[72:75], v10, s[12:13]
	s_add_u32 s12, s12, 0x8000
	s_addc_u32 s13, s13, 0
	global_load_dwordx4 v[76:79], v10, s[12:13]
	s_add_u32 s12, s12, 0x8000
	s_addc_u32 s13, s13, 0
	global_load_dwordx4 v[80:83], v10, s[12:13]
	s_add_u32 s12, s12, 0x8000
	s_addc_u32 s13, s13, 0
	global_load_dwordx4 v[84:87], v10, s[12:13]
	s_add_u32 s12, s12, 0x8000
	s_addc_u32 s13, s13, 0
	global_load_dwordx4 v[88:91], v10, s[12:13]
	s_add_u32 s12, s12, 0x8000
	s_addc_u32 s13, s13, 0
	global_load_dwordx4 v[92:95], v10, s[12:13]
	s_add_u32 s12, s12, 0x8000
	s_addc_u32 s13, s13, 0
	global_load_dwordx4 v[96:99], v10, s[12:13]
	s_add_i32 s17, s16, 480
	s_min_u32 s17, s17, 0xfff
	s_lshr_b32 s18, s17, 5
	s_add_i32 s18, s18, 0
	s_and_b32 s19, s17, 31
	s_lshl_b32 s19, s19, 21
	s_lshl_b32 s18, s18, 7
	s_add_u32 s18, s18, s19
	s_add_u32 s14, s4, s18
	s_addc_u32 s15, s5, 0
	ds_read_b32 v170, v7
	ds_read_b32 v171, v7 offset:512
	ds_read_b32 v172, v7 offset:1024
	ds_read_b32 v173, v7 offset:1536
	ds_read_b32 v174, v7 offset:2048
	ds_read_b32 v175, v7 offset:2560
	ds_read_b32 v176, v7 offset:3072
	ds_read_b32 v177, v7 offset:3584
	ds_read_b32 v196, v7 offset:4096
	ds_read_b32 v197, v7 offset:4608
	ds_read_b32 v198, v7 offset:5120
	ds_read_b32 v199, v7 offset:5632
	ds_read_b32 v200, v7 offset:6144
	ds_read_b32 v201, v7 offset:6656
	ds_read_b32 v202, v7 offset:7168
	ds_read_b32 v203, v7 offset:7680
	s_waitcnt lgkmcnt(0)
	v_max_f32_e32 v170, v170, v170
	v_max_f32_e32 v171, v171, v171
	v_max_f32_e32 v172, v172, v172
	v_max_f32_e32 v173, v173, v173
	v_max_f32_e32 v174, v174, v174
	v_max_f32_e32 v175, v175, v175
	v_max_f32_e32 v176, v176, v176
	v_max_f32_e32 v177, v177, v177
	v_max_f32_e32 v196, v196, v196
	v_max_f32_e32 v197, v197, v197
	v_max_f32_e32 v198, v198, v198
	v_max_f32_e32 v199, v199, v199
	v_max_f32_e32 v200, v200, v200
	v_max_f32_e32 v201, v201, v201
	v_max_f32_e32 v202, v202, v202
	v_max_f32_e32 v203, v203, v203
	v_med3_f32 v170, v170, s20, v13
	v_med3_f32 v171, v171, s20, v13
	v_med3_f32 v172, v172, s20, v13
	v_med3_f32 v173, v173, s20, v13
	v_med3_f32 v174, v174, s20, v13
	v_med3_f32 v175, v175, s20, v13
	v_med3_f32 v176, v176, s20, v13
	v_med3_f32 v177, v177, s20, v13
	v_med3_f32 v196, v196, s20, v13
	v_med3_f32 v197, v197, s20, v13
	v_med3_f32 v198, v198, s20, v13
	v_med3_f32 v199, v199, s20, v13
	v_med3_f32 v200, v200, s20, v13
	v_med3_f32 v201, v201, s20, v13
	v_med3_f32 v202, v202, s20, v13
	v_med3_f32 v203, v203, s20, v13
	v_mov_b32_e32 v208, 0
	v_mov_b32_e32 v209, 0
	v_mov_b32_e32 v210, 0
	v_mov_b32_e32 v211, 0
	v_cvt_pk_fp8_f32 v208, v170, v171
	v_cvt_pk_fp8_f32 v209, v174, v175
	v_cvt_pk_fp8_f32 v210, v196, v197
	v_cvt_pk_fp8_f32 v211, v200, v201
	v_cvt_pk_fp8_f32 v208, v172, v173 op_sel:[0,0,1]
	v_cvt_pk_fp8_f32 v209, v176, v177 op_sel:[0,0,1]
	v_cvt_pk_fp8_f32 v210, v198, v199 op_sel:[0,0,1]
	v_cvt_pk_fp8_f32 v211, v202, v203 op_sel:[0,0,1]
	s_nop 0
	global_store_dwordx4 v11, v[208:211], s[14:15]
	ds_read_b32 v170, v9
	ds_read_b32 v171, v9 offset:512
	ds_read_b32 v172, v9 offset:1024
	ds_read_b32 v173, v9 offset:1536
	ds_read_b32 v174, v9 offset:2048
	ds_read_b32 v175, v9 offset:2560
	ds_read_b32 v176, v9 offset:3072
	ds_read_b32 v177, v9 offset:3584
	ds_read_b32 v196, v9 offset:4096
	ds_read_b32 v197, v9 offset:4608
	ds_read_b32 v198, v9 offset:5120
	ds_read_b32 v199, v9 offset:5632
	ds_read_b32 v200, v9 offset:6144
	ds_read_b32 v201, v9 offset:6656
	ds_read_b32 v202, v9 offset:7168
	ds_read_b32 v203, v9 offset:7680
	s_waitcnt lgkmcnt(0)
	v_max_f32_e32 v170, v170, v170
	v_max_f32_e32 v171, v171, v171
	v_max_f32_e32 v172, v172, v172
	v_max_f32_e32 v173, v173, v173
	v_max_f32_e32 v174, v174, v174
	v_max_f32_e32 v175, v175, v175
	v_max_f32_e32 v176, v176, v176
	v_max_f32_e32 v177, v177, v177
	v_max_f32_e32 v196, v196, v196
	v_max_f32_e32 v197, v197, v197
	v_max_f32_e32 v198, v198, v198
	v_max_f32_e32 v199, v199, v199
	v_max_f32_e32 v200, v200, v200
	v_max_f32_e32 v201, v201, v201
	v_max_f32_e32 v202, v202, v202
	v_max_f32_e32 v203, v203, v203
	v_med3_f32 v170, v170, s20, v13
	v_med3_f32 v171, v171, s20, v13
	v_med3_f32 v172, v172, s20, v13
	v_med3_f32 v173, v173, s20, v13
	v_med3_f32 v174, v174, s20, v13
	v_med3_f32 v175, v175, s20, v13
	v_med3_f32 v176, v176, s20, v13
	v_med3_f32 v177, v177, s20, v13
	v_med3_f32 v196, v196, s20, v13
	v_med3_f32 v197, v197, s20, v13
	v_med3_f32 v198, v198, s20, v13
	v_med3_f32 v199, v199, s20, v13
	v_med3_f32 v200, v200, s20, v13
	v_med3_f32 v201, v201, s20, v13
	v_med3_f32 v202, v202, s20, v13
	v_med3_f32 v203, v203, s20, v13
	v_mov_b32_e32 v208, 0
	v_mov_b32_e32 v209, 0
	v_mov_b32_e32 v210, 0
	v_mov_b32_e32 v211, 0
	v_cvt_pk_fp8_f32 v208, v170, v171
	v_cvt_pk_fp8_f32 v209, v174, v175
	v_cvt_pk_fp8_f32 v210, v196, v197
	v_cvt_pk_fp8_f32 v211, v200, v201
	v_cvt_pk_fp8_f32 v208, v172, v173 op_sel:[0,0,1]
	v_cvt_pk_fp8_f32 v209, v176, v177 op_sel:[0,0,1]
	v_cvt_pk_fp8_f32 v210, v198, v199 op_sel:[0,0,1]
	v_cvt_pk_fp8_f32 v211, v202, v203 op_sel:[0,0,1]
	s_nop 0
	global_store_dwordx4 v12, v[208:211], s[14:15]
	s_waitcnt vmcnt(32)
	v_mul_f32_e32 v100, 0x43000000, v100
	v_mul_f32_e32 v101, 0x43000000, v101
	v_mul_f32_e32 v102, 0x43000000, v102
	v_mul_f32_e32 v103, 0x43000000, v103
	ds_write_b128 v4, v[100:103]
	v_mul_f32_e32 v104, 0x43000000, v104
	v_mul_f32_e32 v105, 0x43000000, v105
	v_mul_f32_e32 v106, 0x43000000, v106
	v_mul_f32_e32 v107, 0x43000000, v107
	ds_write_b128 v4, v[104:107] offset:1024
	v_mul_f32_e32 v108, 0x43000000, v108
	v_mul_f32_e32 v109, 0x43000000, v109
	v_mul_f32_e32 v110, 0x43000000, v110
	v_mul_f32_e32 v111, 0x43000000, v111
	ds_write_b128 v4, v[108:111] offset:2048
	v_mul_f32_e32 v112, 0x43000000, v112
	v_mul_f32_e32 v113, 0x43000000, v113
	v_mul_f32_e32 v114, 0x43000000, v114
	v_mul_f32_e32 v115, 0x43000000, v115
	ds_write_b128 v4, v[112:115] offset:3072
	v_mul_f32_e32 v116, 0x43000000, v116
	v_mul_f32_e32 v117, 0x43000000, v117
	v_mul_f32_e32 v118, 0x43000000, v118
	v_mul_f32_e32 v119, 0x43000000, v119
	ds_write_b128 v4, v[116:119] offset:4096
	v_mul_f32_e32 v120, 0x43000000, v120
	v_mul_f32_e32 v121, 0x43000000, v121
	v_mul_f32_e32 v122, 0x43000000, v122
	v_mul_f32_e32 v123, 0x43000000, v123
	ds_write_b128 v4, v[120:123] offset:5120
	v_mul_f32_e32 v124, 0x43000000, v124
	v_mul_f32_e32 v125, 0x43000000, v125
	v_mul_f32_e32 v126, 0x43000000, v126
	v_mul_f32_e32 v127, 0x43000000, v127
	ds_write_b128 v4, v[124:127] offset:6144
	v_mul_f32_e32 v128, 0x43000000, v128
	v_mul_f32_e32 v129, 0x43000000, v129
	v_mul_f32_e32 v130, 0x43000000, v130
	v_mul_f32_e32 v131, 0x43000000, v131
	ds_write_b128 v4, v[128:131] offset:7168
	s_waitcnt lgkmcnt(0)
	s_barrier
; #define GAS __attribute__((address_space(1)))
; #define LAS __attribute__((address_space(3)))
; #define LDS_WAIT() asm volatile("s_waitcnt lgkmcnt(0)" ::: "memory")
; __device__ __forceinline__ unsigned pk4_fp8(float a, float b, float c, float d) {
;     a = fminf(fmaxf(a, -448.f), 448.f); b = fminf(fmaxf(b, -448.f), 448.f); c = fminf(fmaxf(c, -448.f), 448.f); d = fminf(fmaxf(d, -448.f), 448.f);
;     int w = __builtin_amdgcn_cvt_pk_fp8_f32(a, b, 0, false); w = __builtin_amdgcn_cvt_pk_fp8_f32(c, d, w, true); return (unsigned)w; }
;     const int pr = item >> 1, kb = 2 * (pr / nblk) + (item & 1), nb = pr % nblk, k0 = 64 * kb, n0 = 32 * nb;
;     const int nr = n0 + (lane & 31); const int sc = MAP == 1 ? src_col_in(nr) : nr;
;     float v[32];
; #pragma unroll
;     for (int i = 0; i < 32; ++i) v[i] = sc >= 0 ? W[(size_t)(k0 + 2 * i + (lane >> 5)) * Nsrc + sc] : 0.f;
; #pragma unroll
;     for (int i = 0; i < 32; ++i) { const int k = k0 + 2 * i + (lane >> 5); float x = v[i] * wscale; if (KS) x *= (k < ksplit ? ksA[k] : ksB[k - ksplit]); scr[(2 * i + (lane >> 5)) * 33 + (lane & 31)] = x; }
;     LDS_WAIT(); asm volatile("" ::: "memory");
;     const int c = lane & 7;
; #pragma unroll
;     for (int j = 0; j < 4; ++j) { const int n = (lane >> 3) + 8 * j; const LAS float* s = scr + (8 * c) * 33 + n;
;         const unsigned long long o = (unsigned long long)pg8::pk4_fp8(s[0 * 33], s[1 * 33], s[2 * 33], s[3 * 33]) | ((unsigned long long)pg8::pk4_fp8(s[4 * 33], s[5 * 33], s[6 * 33], s[7 * 33]) << 32);
;         *(GAS unsigned long long*)(WT + (size_t)(n0 + n) * K + k0 + 8 * c) = o; }
;     LDS_WAIT(); asm volatile("" ::: "memory");
; }
	s_add_i32 s17, s16, 960
	s_min_u32 s17, s17, 0xfff
	s_lshr_b32 s18, s17, 5
	s_add_i32 s18, s18, 0
	s_and_b32 s19, s17, 31
	s_lshl_b32 s18, s18, 21
	s_lshl_b32 s19, s19, 9
	s_add_u32 s18, s18, s19
	s_add_u32 s12, s2, s18
	s_addc_u32 s13, s3, 0
	global_load_dwordx4 v[100:103], v10, s[12:13]
	s_add_u32 s12, s12, 0x8000
	s_addc_u32 s13, s13, 0
	global_load_dwordx4 v[104:107], v10, s[12:13]
	s_add_u32 s12, s12, 0x8000
	s_addc_u32 s13, s13, 0
	global_load_dwordx4 v[108:111], v10, s[12:13]
	s_add_u32 s12, s12, 0x8000
	s_addc_u32 s13, s13, 0
	global_load_dwordx4 v[112:115], v10, s[12:13]
	s_add_u32 s12, s12, 0x8000
	s_addc_u32 s13, s13, 0
	global_load_dwordx4 v[116:119], v10, s[12:13]
	s_add_u32 s12, s12, 0x8000
	s_addc_u32 s13, s13, 0
	global_load_dwordx4 v[120:123], v10, s[12:13]
	s_add_u32 s12, s12, 0x8000
	s_addc_u32 s13, s13, 0
	global_load_dwordx4 v[124:127], v10, s[12:13]
	s_add_u32 s12, s12, 0x8000
	s_addc_u32 s13, s13, 0
	global_load_dwordx4 v[128:131], v10, s[12:13]
	s_add_i32 s17, s16, 576
	s_min_u32 s17, s17, 0xfff
	s_lshr_b32 s18, s17, 5
	s_add_i32 s18, s18, 0
	s_and_b32 s19, s17, 31
	s_lshl_b32 s19, s19, 21
	s_lshl_b32 s18, s18, 7
	s_add_u32 s18, s18, s19
	s_add_u32 s14, s4, s18
	s_addc_u32 s15, s5, 0
	ds_read_b32 v170, v6
	ds_read_b32 v171, v6 offset:512
	ds_read_b32 v172, v6 offset:1024
	ds_read_b32 v173, v6 offset:1536
	ds_read_b32 v174, v6 offset:2048
	ds_read_b32 v175, v6 offset:2560
	ds_read_b32 v176, v6 offset:3072
	ds_read_b32 v177, v6 offset:3584
	ds_read_b32 v196, v6 offset:4096
	ds_read_b32 v197, v6 offset:4608
	ds_read_b32 v198, v6 offset:5120
	ds_read_b32 v199, v6 offset:5632
	ds_read_b32 v200, v6 offset:6144
	ds_read_b32 v201, v6 offset:6656
	ds_read_b32 v202, v6 offset:7168
	ds_read_b32 v203, v6 offset:7680
	s_waitcnt lgkmcnt(0)
	v_max_f32_e32 v170, v170, v170
	v_max_f32_e32 v171, v171, v171
	v_max_f32_e32 v172, v172, v172
	v_max_f32_e32 v173, v173, v173
	v_max_f32_e32 v174, v174, v174
	v_max_f32_e32 v175, v175, v175
	v_max_f32_e32 v176, v176, v176
	v_max_f32_e32 v177, v177, v177
	v_max_f32_e32 v196, v196, v196
	v_max_f32_e32 v197, v197, v197
	v_max_f32_e32 v198, v198, v198
	v_max_f32_e32 v199, v199, v199
	v_max_f32_e32 v200, v200, v200
	v_max_f32_e32 v201, v201, v201
	v_max_f32_e32 v202, v202, v202
	v_max_f32_e32 v203, v203, v203
	v_med3_f32 v170, v170, s20, v13
	v_med3_f32 v171, v171, s20, v13
	v_med3_f32 v172, v172, s20, v13
	v_med3_f32 v173, v173, s20, v13
	v_med3_f32 v174, v174, s20, v13
	v_med3_f32 v175, v175, s20, v13
	v_med3_f32 v176, v176, s20, v13
	v_med3_f32 v177, v177, s20, v13
	v_med3_f32 v196, v196, s20, v13
	v_med3_f32 v197, v197, s20, v13
	v_med3_f32 v198, v198, s20, v13
	v_med3_f32 v199, v199, s20, v13
	v_med3_f32 v200, v200, s20, v13
	v_med3_f32 v201, v201, s20, v13
	v_med3_f32 v202, v202, s20, v13
	v_med3_f32 v203, v203, s20, v13
	v_mov_b32_e32 v208, 0
	v_mov_b32_e32 v209, 0
	v_mov_b32_e32 v210, 0
	v_mov_b32_e32 v211, 0
	v_cvt_pk_fp8_f32 v208, v170, v171
	v_cvt_pk_fp8_f32 v209, v174, v175
	v_cvt_pk_fp8_f32 v210, v196, v197
	v_cvt_pk_fp8_f32 v211, v200, v201
	v_cvt_pk_fp8_f32 v208, v172, v173 op_sel:[0,0,1]
	v_cvt_pk_fp8_f32 v209, v176, v177 op_sel:[0,0,1]
	v_cvt_pk_fp8_f32 v210, v198, v199 op_sel:[0,0,1]
	v_cvt_pk_fp8_f32 v211, v202, v203 op_sel:[0,0,1]
	s_nop 0
	global_store_dwordx4 v11, v[208:211], s[14:15]
	ds_read_b32 v170, v8
	ds_read_b32 v171, v8 offset:512
	ds_read_b32 v172, v8 offset:1024
	ds_read_b32 v173, v8 offset:1536
	ds_read_b32 v174, v8 offset:2048
	ds_read_b32 v175, v8 offset:2560
	ds_read_b32 v176, v8 offset:3072
	ds_read_b32 v177, v8 offset:3584
	ds_read_b32 v196, v8 offset:4096
	ds_read_b32 v197, v8 offset:4608
	ds_read_b32 v198, v8 offset:5120
	ds_read_b32 v199, v8 offset:5632
	ds_read_b32 v200, v8 offset:6144
	ds_read_b32 v201, v8 offset:6656
	ds_read_b32 v202, v8 offset:7168
	ds_read_b32 v203, v8 offset:7680
	s_waitcnt lgkmcnt(0)
	v_max_f32_e32 v170, v170, v170
	v_max_f32_e32 v171, v171, v171
	v_max_f32_e32 v172, v172, v172
	v_max_f32_e32 v173, v173, v173
	v_max_f32_e32 v174, v174, v174
	v_max_f32_e32 v175, v175, v175
	v_max_f32_e32 v176, v176, v176
	v_max_f32_e32 v177, v177, v177
	v_max_f32_e32 v196, v196, v196
	v_max_f32_e32 v197, v197, v197
	v_max_f32_e32 v198, v198, v198
	v_max_f32_e32 v199, v199, v199
	v_max_f32_e32 v200, v200, v200
	v_max_f32_e32 v201, v201, v201
	v_max_f32_e32 v202, v202, v202
	v_max_f32_e32 v203, v203, v203
	v_med3_f32 v170, v170, s20, v13
	v_med3_f32 v171, v171, s20, v13
	v_med3_f32 v172, v172, s20, v13
	v_med3_f32 v173, v173, s20, v13
	v_med3_f32 v174, v174, s20, v13
	v_med3_f32 v175, v175, s20, v13
	v_med3_f32 v176, v176, s20, v13
	v_med3_f32 v177, v177, s20, v13
	v_med3_f32 v196, v196, s20, v13
	v_med3_f32 v197, v197, s20, v13
	v_med3_f32 v198, v198, s20, v13
	v_med3_f32 v199, v199, s20, v13
	v_med3_f32 v200, v200, s20, v13
	v_med3_f32 v201, v201, s20, v13
	v_med3_f32 v202, v202, s20, v13
	v_med3_f32 v203, v203, s20, v13
	v_mov_b32_e32 v208, 0
	v_mov_b32_e32 v209, 0
	v_mov_b32_e32 v210, 0
	v_mov_b32_e32 v211, 0
	v_cvt_pk_fp8_f32 v208, v170, v171
	v_cvt_pk_fp8_f32 v209, v174, v175
	v_cvt_pk_fp8_f32 v210, v196, v197
	v_cvt_pk_fp8_f32 v211, v200, v201
	v_cvt_pk_fp8_f32 v208, v172, v173 op_sel:[0,0,1]
	v_cvt_pk_fp8_f32 v209, v176, v177 op_sel:[0,0,1]
	v_cvt_pk_fp8_f32 v210, v198, v199 op_sel:[0,0,1]
	v_cvt_pk_fp8_f32 v211, v202, v203 op_sel:[0,0,1]
	s_nop 0
	global_store_dwordx4 v12, v[208:211], s[14:15]
	s_waitcnt vmcnt(32)
	v_mul_f32_e32 v132, 0x43000000, v132
	v_mul_f32_e32 v133, 0x43000000, v133
	v_mul_f32_e32 v134, 0x43000000, v134
	v_mul_f32_e32 v135, 0x43000000, v135
	ds_write_b128 v5, v[132:135]
	v_mul_f32_e32 v136, 0x43000000, v136
	v_mul_f32_e32 v137, 0x43000000, v137
	v_mul_f32_e32 v138, 0x43000000, v138
	v_mul_f32_e32 v139, 0x43000000, v139
	ds_write_b128 v5, v[136:139] offset:1024
	v_mul_f32_e32 v140, 0x43000000, v140
	v_mul_f32_e32 v141, 0x43000000, v141
	v_mul_f32_e32 v142, 0x43000000, v142
	v_mul_f32_e32 v143, 0x43000000, v143
	ds_write_b128 v5, v[140:143] offset:2048
	v_mul_f32_e32 v144, 0x43000000, v144
	v_mul_f32_e32 v145, 0x43000000, v145
	v_mul_f32_e32 v146, 0x43000000, v146
	v_mul_f32_e32 v147, 0x43000000, v147
	ds_write_b128 v5, v[144:147] offset:3072
	v_mul_f32_e32 v148, 0x43000000, v148
	v_mul_f32_e32 v149, 0x43000000, v149
	v_mul_f32_e32 v150, 0x43000000, v150
	v_mul_f32_e32 v151, 0x43000000, v151
	ds_write_b128 v5, v[148:151] offset:4096
	v_mul_f32_e32 v152, 0x43000000, v152
	v_mul_f32_e32 v153, 0x43000000, v153
	v_mul_f32_e32 v154, 0x43000000, v154
	v_mul_f32_e32 v155, 0x43000000, v155
	ds_write_b128 v5, v[152:155] offset:5120
	v_mul_f32_e32 v156, 0x43000000, v156
	v_mul_f32_e32 v157, 0x43000000, v157
	v_mul_f32_e32 v158, 0x43000000, v158
	v_mul_f32_e32 v159, 0x43000000, v159
	ds_write_b128 v5, v[156:159] offset:6144
	v_mul_f32_e32 v160, 0x43000000, v160
	v_mul_f32_e32 v161, 0x43000000, v161
	v_mul_f32_e32 v162, 0x43000000, v162
	v_mul_f32_e32 v163, 0x43000000, v163
	ds_write_b128 v5, v[160:163] offset:7168
	s_waitcnt lgkmcnt(0)
	s_barrier
; #define GAS __attribute__((address_space(1)))
; #define LAS __attribute__((address_space(3)))
; #define LDS_WAIT() asm volatile("s_waitcnt lgkmcnt(0)" ::: "memory")
; __device__ __forceinline__ unsigned pk4_fp8(float a, float b, float c, float d) {
;     a = fminf(fmaxf(a, -448.f), 448.f); b = fminf(fmaxf(b, -448.f), 448.f); c = fminf(fmaxf(c, -448.f), 448.f); d = fminf(fmaxf(d, -448.f), 448.f);
;     int w = __builtin_amdgcn_cvt_pk_fp8_f32(a, b, 0, false); w = __builtin_amdgcn_cvt_pk_fp8_f32(c, d, w, true); return (unsigned)w; }
;     const int pr = item >> 1, kb = 2 * (pr / nblk) + (item & 1), nb = pr % nblk, k0 = 64 * kb, n0 = 32 * nb;
;     const int nr = n0 + (lane & 31); const int sc = MAP == 1 ? src_col_in(nr) : nr;
;     float v[32];
; #pragma unroll
;     for (int i = 0; i < 32; ++i) v[i] = sc >= 0 ? W[(size_t)(k0 + 2 * i + (lane >> 5)) * Nsrc + sc] : 0.f;
; #pragma unroll
;     for (int i = 0; i < 32; ++i) { const int k = k0 + 2 * i + (lane >> 5); float x = v[i] * wscale; if (KS) x *= (k < ksplit ? ksA[k] : ksB[k - ksplit]); scr[(2 * i + (lane >> 5)) * 33 + (lane & 31)] = x; }
;     LDS_WAIT(); asm volatile("" ::: "memory");
;     const int c = lane & 7;
; #pragma unroll
;     for (int j = 0; j < 4; ++j) { const int n = (lane >> 3) + 8 * j; const LAS float* s = scr + (8 * c) * 33 + n;
;         const unsigned long long o = (unsigned long long)pg8::pk4_fp8(s[0 * 33], s[1 * 33], s[2 * 33], s[3 * 33]) | ((unsigned long long)pg8::pk4_fp8(s[4 * 33], s[5 * 33], s[6 * 33], s[7 * 33]) << 32);
;         *(GAS unsigned long long*)(WT + (size_t)(n0 + n) * K + k0 + 8 * c) = o; }
;     LDS_WAIT(); asm volatile("" ::: "memory");
; }
	s_add_i32 s17, s16, 1056
	s_min_u32 s17, s17, 0xfff
	s_lshr_b32 s18, s17, 5
	s_add_i32 s18, s18, 0
	s_and_b32 s19, s17, 31
	s_lshl_b32 s18, s18, 21
	s_lshl_b32 s19, s19, 9
	s_add_u32 s18, s18, s19
	s_add_u32 s12, s2, s18
	s_addc_u32 s13, s3, 0
	global_load_dwordx4 v[132:135], v10, s[12:13]
	s_add_u32 s12, s12, 0x8000
	s_addc_u32 s13, s13, 0
	global_load_dwordx4 v[136:139], v10, s[12:13]
	s_add_u32 s12, s12, 0x8000
	s_addc_u32 s13, s13, 0
	global_load_dwordx4 v[140:143], v10, s[12:13]
	s_add_u32 s12, s12, 0x8000
	s_addc_u32 s13, s13, 0
	global_load_dwordx4 v[144:147], v10, s[12:13]
	s_add_u32 s12, s12, 0x8000
	s_addc_u32 s13, s13, 0
	global_load_dwordx4 v[148:151], v10, s[12:13]
	s_add_u32 s12, s12, 0x8000
	s_addc_u32 s13, s13, 0
	global_load_dwordx4 v[152:155], v10, s[12:13]
	s_add_u32 s12, s12, 0x8000
	s_addc_u32 s13, s13, 0
	global_load_dwordx4 v[156:159], v10, s[12:13]
	s_add_u32 s12, s12, 0x8000
	s_addc_u32 s13, s13, 0
	global_load_dwordx4 v[160:163], v10, s[12:13]
	s_add_i32 s17, s16, 672
	s_min_u32 s17, s17, 0xfff
	s_lshr_b32 s18, s17, 5
	s_add_i32 s18, s18, 0
	s_and_b32 s19, s17, 31
	s_lshl_b32 s19, s19, 21
	s_lshl_b32 s18, s18, 7
	s_add_u32 s18, s18, s19
	s_add_u32 s14, s4, s18
	s_addc_u32 s15, s5, 0
	ds_read_b32 v170, v7
	ds_read_b32 v171, v7 offset:512
	ds_read_b32 v172, v7 offset:1024
	ds_read_b32 v173, v7 offset:1536
	ds_read_b32 v174, v7 offset:2048
	ds_read_b32 v175, v7 offset:2560
	ds_read_b32 v176, v7 offset:3072
	ds_read_b32 v177, v7 offset:3584
	ds_read_b32 v196, v7 offset:4096
	ds_read_b32 v197, v7 offset:4608
	ds_read_b32 v198, v7 offset:5120
	ds_read_b32 v199, v7 offset:5632
	ds_read_b32 v200, v7 offset:6144
	ds_read_b32 v201, v7 offset:6656
	ds_read_b32 v202, v7 offset:7168
	ds_read_b32 v203, v7 offset:7680
	s_waitcnt lgkmcnt(0)
	v_max_f32_e32 v170, v170, v170
	v_max_f32_e32 v171, v171, v171
	v_max_f32_e32 v172, v172, v172
	v_max_f32_e32 v173, v173, v173
	v_max_f32_e32 v174, v174, v174
	v_max_f32_e32 v175, v175, v175
	v_max_f32_e32 v176, v176, v176
	v_max_f32_e32 v177, v177, v177
	v_max_f32_e32 v196, v196, v196
	v_max_f32_e32 v197, v197, v197
	v_max_f32_e32 v198, v198, v198
	v_max_f32_e32 v199, v199, v199
	v_max_f32_e32 v200, v200, v200
	v_max_f32_e32 v201, v201, v201
	v_max_f32_e32 v202, v202, v202
	v_max_f32_e32 v203, v203, v203
	v_med3_f32 v170, v170, s20, v13
	v_med3_f32 v171, v171, s20, v13
	v_med3_f32 v172, v172, s20, v13
	v_med3_f32 v173, v173, s20, v13
	v_med3_f32 v174, v174, s20, v13
	v_med3_f32 v175, v175, s20, v13
	v_med3_f32 v176, v176, s20, v13
	v_med3_f32 v177, v177, s20, v13
	v_med3_f32 v196, v196, s20, v13
	v_med3_f32 v197, v197, s20, v13
	v_med3_f32 v198, v198, s20, v13
	v_med3_f32 v199, v199, s20, v13
	v_med3_f32 v200, v200, s20, v13
	v_med3_f32 v201, v201, s20, v13
	v_med3_f32 v202, v202, s20, v13
	v_med3_f32 v203, v203, s20, v13
	v_mov_b32_e32 v208, 0
	v_mov_b32_e32 v209, 0
	v_mov_b32_e32 v210, 0
	v_mov_b32_e32 v211, 0
	v_cvt_pk_fp8_f32 v208, v170, v171
	v_cvt_pk_fp8_f32 v209, v174, v175
	v_cvt_pk_fp8_f32 v210, v196, v197
	v_cvt_pk_fp8_f32 v211, v200, v201
	v_cvt_pk_fp8_f32 v208, v172, v173 op_sel:[0,0,1]
	v_cvt_pk_fp8_f32 v209, v176, v177 op_sel:[0,0,1]
	v_cvt_pk_fp8_f32 v210, v198, v199 op_sel:[0,0,1]
	v_cvt_pk_fp8_f32 v211, v202, v203 op_sel:[0,0,1]
	s_nop 0
	global_store_dwordx4 v11, v[208:211], s[14:15]
	ds_read_b32 v170, v9
	ds_read_b32 v171, v9 offset:512
	ds_read_b32 v172, v9 offset:1024
	ds_read_b32 v173, v9 offset:1536
	ds_read_b32 v174, v9 offset:2048
	ds_read_b32 v175, v9 offset:2560
	ds_read_b32 v176, v9 offset:3072
	ds_read_b32 v177, v9 offset:3584
	ds_read_b32 v196, v9 offset:4096
	ds_read_b32 v197, v9 offset:4608
	ds_read_b32 v198, v9 offset:5120
	ds_read_b32 v199, v9 offset:5632
	ds_read_b32 v200, v9 offset:6144
	ds_read_b32 v201, v9 offset:6656
	ds_read_b32 v202, v9 offset:7168
	ds_read_b32 v203, v9 offset:7680
	s_waitcnt lgkmcnt(0)
	v_max_f32_e32 v170, v170, v170
	v_max_f32_e32 v171, v171, v171
	v_max_f32_e32 v172, v172, v172
	v_max_f32_e32 v173, v173, v173
	v_max_f32_e32 v174, v174, v174
	v_max_f32_e32 v175, v175, v175
	v_max_f32_e32 v176, v176, v176
	v_max_f32_e32 v177, v177, v177
	v_max_f32_e32 v196, v196, v196
	v_max_f32_e32 v197, v197, v197
	v_max_f32_e32 v198, v198, v198
	v_max_f32_e32 v199, v199, v199
	v_max_f32_e32 v200, v200, v200
	v_max_f32_e32 v201, v201, v201
	v_max_f32_e32 v202, v202, v202
	v_max_f32_e32 v203, v203, v203
	v_med3_f32 v170, v170, s20, v13
	v_med3_f32 v171, v171, s20, v13
	v_med3_f32 v172, v172, s20, v13
	v_med3_f32 v173, v173, s20, v13
	v_med3_f32 v174, v174, s20, v13
	v_med3_f32 v175, v175, s20, v13
	v_med3_f32 v176, v176, s20, v13
	v_med3_f32 v177, v177, s20, v13
	v_med3_f32 v196, v196, s20, v13
	v_med3_f32 v197, v197, s20, v13
	v_med3_f32 v198, v198, s20, v13
	v_med3_f32 v199, v199, s20, v13
	v_med3_f32 v200, v200, s20, v13
	v_med3_f32 v201, v201, s20, v13
	v_med3_f32 v202, v202, s20, v13
	v_med3_f32 v203, v203, s20, v13
	v_mov_b32_e32 v208, 0
	v_mov_b32_e32 v209, 0
	v_mov_b32_e32 v210, 0
	v_mov_b32_e32 v211, 0
	v_cvt_pk_fp8_f32 v208, v170, v171
	v_cvt_pk_fp8_f32 v209, v174, v175
	v_cvt_pk_fp8_f32 v210, v196, v197
	v_cvt_pk_fp8_f32 v211, v200, v201
	v_cvt_pk_fp8_f32 v208, v172, v173 op_sel:[0,0,1]
	v_cvt_pk_fp8_f32 v209, v176, v177 op_sel:[0,0,1]
	v_cvt_pk_fp8_f32 v210, v198, v199 op_sel:[0,0,1]
	v_cvt_pk_fp8_f32 v211, v202, v203 op_sel:[0,0,1]
	s_nop 0
	global_store_dwordx4 v12, v[208:211], s[14:15]
	s_waitcnt vmcnt(32)
	v_mul_f32_e32 v36, 0x43000000, v36
	v_mul_f32_e32 v37, 0x43000000, v37
	v_mul_f32_e32 v38, 0x43000000, v38
	v_mul_f32_e32 v39, 0x43000000, v39
	ds_write_b128 v4, v[36:39]
	v_mul_f32_e32 v40, 0x43000000, v40
	v_mul_f32_e32 v41, 0x43000000, v41
	v_mul_f32_e32 v42, 0x43000000, v42
	v_mul_f32_e32 v43, 0x43000000, v43
	ds_write_b128 v4, v[40:43] offset:1024
	v_mul_f32_e32 v44, 0x43000000, v44
	v_mul_f32_e32 v45, 0x43000000, v45
	v_mul_f32_e32 v46, 0x43000000, v46
	v_mul_f32_e32 v47, 0x43000000, v47
	ds_write_b128 v4, v[44:47] offset:2048
	v_mul_f32_e32 v48, 0x43000000, v48
	v_mul_f32_e32 v49, 0x43000000, v49
	v_mul_f32_e32 v50, 0x43000000, v50
	v_mul_f32_e32 v51, 0x43000000, v51
	ds_write_b128 v4, v[48:51] offset:3072
	v_mul_f32_e32 v52, 0x43000000, v52
	v_mul_f32_e32 v53, 0x43000000, v53
	v_mul_f32_e32 v54, 0x43000000, v54
	v_mul_f32_e32 v55, 0x43000000, v55
	ds_write_b128 v4, v[52:55] offset:4096
	v_mul_f32_e32 v56, 0x43000000, v56
	v_mul_f32_e32 v57, 0x43000000, v57
	v_mul_f32_e32 v58, 0x43000000, v58
	v_mul_f32_e32 v59, 0x43000000, v59
	ds_write_b128 v4, v[56:59] offset:5120
	v_mul_f32_e32 v60, 0x43000000, v60
	v_mul_f32_e32 v61, 0x43000000, v61
	v_mul_f32_e32 v62, 0x43000000, v62
	v_mul_f32_e32 v63, 0x43000000, v63
	ds_write_b128 v4, v[60:63] offset:6144
	v_mul_f32_e32 v64, 0x43000000, v64
	v_mul_f32_e32 v65, 0x43000000, v65
	v_mul_f32_e32 v66, 0x43000000, v66
	v_mul_f32_e32 v67, 0x43000000, v67
	ds_write_b128 v4, v[64:67] offset:7168
	s_waitcnt lgkmcnt(0)
	s_barrier
; #define GAS __attribute__((address_space(1)))
; #define LAS __attribute__((address_space(3)))
; #define LDS_WAIT() asm volatile("s_waitcnt lgkmcnt(0)" ::: "memory")
; __device__ __forceinline__ unsigned pk4_fp8(float a, float b, float c, float d) {
;     a = fminf(fmaxf(a, -448.f), 448.f); b = fminf(fmaxf(b, -448.f), 448.f); c = fminf(fmaxf(c, -448.f), 448.f); d = fminf(fmaxf(d, -448.f), 448.f);
;     int w = __builtin_amdgcn_cvt_pk_fp8_f32(a, b, 0, false); w = __builtin_amdgcn_cvt_pk_fp8_f32(c, d, w, true); return (unsigned)w; }
;     const int pr = item >> 1, kb = 2 * (pr / nblk) + (item & 1), nb = pr % nblk, k0 = 64 * kb, n0 = 32 * nb;
;     const int nr = n0 + (lane & 31); const int sc = MAP == 1 ? src_col_in(nr) : nr;
;     float v[32];
; #pragma unroll
;     for (int i = 0; i < 32; ++i) v[i] = sc >= 0 ? W[(size_t)(k0 + 2 * i + (lane >> 5)) * Nsrc + sc] : 0.f;
; #pragma unroll
;     for (int i = 0; i < 32; ++i) { const int k = k0 + 2 * i + (lane >> 5); float x = v[i] * wscale; if (KS) x *= (k < ksplit ? ksA[k] : ksB[k - ksplit]); scr[(2 * i + (lane >> 5)) * 33 + (lane & 31)] = x; }
;     LDS_WAIT(); asm volatile("" ::: "memory");
;     const int c = lane & 7;
; #pragma unroll
;     for (int j = 0; j < 4; ++j) { const int n = (lane >> 3) + 8 * j; const LAS float* s = scr + (8 * c) * 33 + n;
;         const unsigned long long o = (unsigned long long)pg8::pk4_fp8(s[0 * 33], s[1 * 33], s[2 * 33], s[3 * 33]) | ((unsigned long long)pg8::pk4_fp8(s[4 * 33], s[5 * 33], s[6 * 33], s[7 * 33]) << 32);
;         *(GAS unsigned long long*)(WT + (size_t)(n0 + n) * K + k0 + 8 * c) = o; }
;     LDS_WAIT(); asm volatile("" ::: "memory");
; }
	s_add_i32 s17, s16, 1152
	s_min_u32 s17, s17, 0xfff
	s_lshr_b32 s18, s17, 5
	s_add_i32 s18, s18, 0
	s_and_b32 s19, s17, 31
	s_lshl_b32 s18, s18, 21
	s_lshl_b32 s19, s19, 9
	s_add_u32 s18, s18, s19
	s_add_u32 s12, s2, s18
	s_addc_u32 s13, s3, 0
	global_load_dwordx4 v[36:39], v10, s[12:13]
	s_add_u32 s12, s12, 0x8000
	s_addc_u32 s13, s13, 0
	global_load_dwordx4 v[40:43], v10, s[12:13]
	s_add_u32 s12, s12, 0x8000
	s_addc_u32 s13, s13, 0
	global_load_dwordx4 v[44:47], v10, s[12:13]
	s_add_u32 s12, s12, 0x8000
	s_addc_u32 s13, s13, 0
	global_load_dwordx4 v[48:51], v10, s[12:13]
	s_add_u32 s12, s12, 0x8000
	s_addc_u32 s13, s13, 0
	global_load_dwordx4 v[52:55], v10, s[12:13]
	s_add_u32 s12, s12, 0x8000
	s_addc_u32 s13, s13, 0
	global_load_dwordx4 v[56:59], v10, s[12:13]
	s_add_u32 s12, s12, 0x8000
	s_addc_u32 s13, s13, 0
	global_load_dwordx4 v[60:63], v10, s[12:13]
	s_add_u32 s12, s12, 0x8000
	s_addc_u32 s13, s13, 0
	global_load_dwordx4 v[64:67], v10, s[12:13]
	s_add_i32 s17, s16, 768
	s_min_u32 s17, s17, 0xfff
	s_lshr_b32 s18, s17, 5
	s_add_i32 s18, s18, 0
	s_and_b32 s19, s17, 31
	s_lshl_b32 s19, s19, 21
	s_lshl_b32 s18, s18, 7
	s_add_u32 s18, s18, s19
	s_add_u32 s14, s4, s18
	s_addc_u32 s15, s5, 0
	ds_read_b32 v170, v6
	ds_read_b32 v171, v6 offset:512
	ds_read_b32 v172, v6 offset:1024
	ds_read_b32 v173, v6 offset:1536
	ds_read_b32 v174, v6 offset:2048
	ds_read_b32 v175, v6 offset:2560
	ds_read_b32 v176, v6 offset:3072
	ds_read_b32 v177, v6 offset:3584
	ds_read_b32 v196, v6 offset:4096
	ds_read_b32 v197, v6 offset:4608
	ds_read_b32 v198, v6 offset:5120
	ds_read_b32 v199, v6 offset:5632
	ds_read_b32 v200, v6 offset:6144
	ds_read_b32 v201, v6 offset:6656
	ds_read_b32 v202, v6 offset:7168
	ds_read_b32 v203, v6 offset:7680
	s_waitcnt lgkmcnt(0)
	v_max_f32_e32 v170, v170, v170
	v_max_f32_e32 v171, v171, v171
	v_max_f32_e32 v172, v172, v172
	v_max_f32_e32 v173, v173, v173
	v_max_f32_e32 v174, v174, v174
	v_max_f32_e32 v175, v175, v175
	v_max_f32_e32 v176, v176, v176
	v_max_f32_e32 v177, v177, v177
	v_max_f32_e32 v196, v196, v196
	v_max_f32_e32 v197, v197, v197
	v_max_f32_e32 v198, v198, v198
	v_max_f32_e32 v199, v199, v199
	v_max_f32_e32 v200, v200, v200
	v_max_f32_e32 v201, v201, v201
	v_max_f32_e32 v202, v202, v202
	v_max_f32_e32 v203, v203, v203
	v_med3_f32 v170, v170, s20, v13
	v_med3_f32 v171, v171, s20, v13
	v_med3_f32 v172, v172, s20, v13
	v_med3_f32 v173, v173, s20, v13
	v_med3_f32 v174, v174, s20, v13
	v_med3_f32 v175, v175, s20, v13
	v_med3_f32 v176, v176, s20, v13
	v_med3_f32 v177, v177, s20, v13
	v_med3_f32 v196, v196, s20, v13
	v_med3_f32 v197, v197, s20, v13
	v_med3_f32 v198, v198, s20, v13
	v_med3_f32 v199, v199, s20, v13
	v_med3_f32 v200, v200, s20, v13
	v_med3_f32 v201, v201, s20, v13
	v_med3_f32 v202, v202, s20, v13
	v_med3_f32 v203, v203, s20, v13
	v_mov_b32_e32 v208, 0
	v_mov_b32_e32 v209, 0
	v_mov_b32_e32 v210, 0
	v_mov_b32_e32 v211, 0
	v_cvt_pk_fp8_f32 v208, v170, v171
	v_cvt_pk_fp8_f32 v209, v174, v175
	v_cvt_pk_fp8_f32 v210, v196, v197
	v_cvt_pk_fp8_f32 v211, v200, v201
	v_cvt_pk_fp8_f32 v208, v172, v173 op_sel:[0,0,1]
	v_cvt_pk_fp8_f32 v209, v176, v177 op_sel:[0,0,1]
	v_cvt_pk_fp8_f32 v210, v198, v199 op_sel:[0,0,1]
	v_cvt_pk_fp8_f32 v211, v202, v203 op_sel:[0,0,1]
	s_nop 0
	global_store_dwordx4 v11, v[208:211], s[14:15]
	ds_read_b32 v170, v8
	ds_read_b32 v171, v8 offset:512
	ds_read_b32 v172, v8 offset:1024
	ds_read_b32 v173, v8 offset:1536
	ds_read_b32 v174, v8 offset:2048
	ds_read_b32 v175, v8 offset:2560
	ds_read_b32 v176, v8 offset:3072
	ds_read_b32 v177, v8 offset:3584
	ds_read_b32 v196, v8 offset:4096
	ds_read_b32 v197, v8 offset:4608
	ds_read_b32 v198, v8 offset:5120
	ds_read_b32 v199, v8 offset:5632
	ds_read_b32 v200, v8 offset:6144
	ds_read_b32 v201, v8 offset:6656
	ds_read_b32 v202, v8 offset:7168
	ds_read_b32 v203, v8 offset:7680
	s_waitcnt lgkmcnt(0)
	v_max_f32_e32 v170, v170, v170
	v_max_f32_e32 v171, v171, v171
	v_max_f32_e32 v172, v172, v172
	v_max_f32_e32 v173, v173, v173
	v_max_f32_e32 v174, v174, v174
	v_max_f32_e32 v175, v175, v175
	v_max_f32_e32 v176, v176, v176
	v_max_f32_e32 v177, v177, v177
	v_max_f32_e32 v196, v196, v196
	v_max_f32_e32 v197, v197, v197
	v_max_f32_e32 v198, v198, v198
	v_max_f32_e32 v199, v199, v199
	v_max_f32_e32 v200, v200, v200
	v_max_f32_e32 v201, v201, v201
	v_max_f32_e32 v202, v202, v202
	v_max_f32_e32 v203, v203, v203
	v_med3_f32 v170, v170, s20, v13
	v_med3_f32 v171, v171, s20, v13
	v_med3_f32 v172, v172, s20, v13
	v_med3_f32 v173, v173, s20, v13
	v_med3_f32 v174, v174, s20, v13
	v_med3_f32 v175, v175, s20, v13
	v_med3_f32 v176, v176, s20, v13
	v_med3_f32 v177, v177, s20, v13
	v_med3_f32 v196, v196, s20, v13
	v_med3_f32 v197, v197, s20, v13
	v_med3_f32 v198, v198, s20, v13
	v_med3_f32 v199, v199, s20, v13
	v_med3_f32 v200, v200, s20, v13
	v_med3_f32 v201, v201, s20, v13
	v_med3_f32 v202, v202, s20, v13
	v_med3_f32 v203, v203, s20, v13
	v_mov_b32_e32 v208, 0
	v_mov_b32_e32 v209, 0
	v_mov_b32_e32 v210, 0
	v_mov_b32_e32 v211, 0
	v_cvt_pk_fp8_f32 v208, v170, v171
	v_cvt_pk_fp8_f32 v209, v174, v175
	v_cvt_pk_fp8_f32 v210, v196, v197
	v_cvt_pk_fp8_f32 v211, v200, v201
	v_cvt_pk_fp8_f32 v208, v172, v173 op_sel:[0,0,1]
	v_cvt_pk_fp8_f32 v209, v176, v177 op_sel:[0,0,1]
	v_cvt_pk_fp8_f32 v210, v198, v199 op_sel:[0,0,1]
	v_cvt_pk_fp8_f32 v211, v202, v203 op_sel:[0,0,1]
	s_nop 0
	global_store_dwordx4 v12, v[208:211], s[14:15]
	s_waitcnt vmcnt(32)
	v_mul_f32_e32 v68, 0x43000000, v68
	v_mul_f32_e32 v69, 0x43000000, v69
	v_mul_f32_e32 v70, 0x43000000, v70
	v_mul_f32_e32 v71, 0x43000000, v71
	ds_write_b128 v5, v[68:71]
	v_mul_f32_e32 v72, 0x43000000, v72
	v_mul_f32_e32 v73, 0x43000000, v73
	v_mul_f32_e32 v74, 0x43000000, v74
	v_mul_f32_e32 v75, 0x43000000, v75
	ds_write_b128 v5, v[72:75] offset:1024
	v_mul_f32_e32 v76, 0x43000000, v76
	v_mul_f32_e32 v77, 0x43000000, v77
	v_mul_f32_e32 v78, 0x43000000, v78
	v_mul_f32_e32 v79, 0x43000000, v79
	ds_write_b128 v5, v[76:79] offset:2048
	v_mul_f32_e32 v80, 0x43000000, v80
	v_mul_f32_e32 v81, 0x43000000, v81
	v_mul_f32_e32 v82, 0x43000000, v82
	v_mul_f32_e32 v83, 0x43000000, v83
	ds_write_b128 v5, v[80:83] offset:3072
	v_mul_f32_e32 v84, 0x43000000, v84
	v_mul_f32_e32 v85, 0x43000000, v85
	v_mul_f32_e32 v86, 0x43000000, v86
	v_mul_f32_e32 v87, 0x43000000, v87
	ds_write_b128 v5, v[84:87] offset:4096
	v_mul_f32_e32 v88, 0x43000000, v88
	v_mul_f32_e32 v89, 0x43000000, v89
	v_mul_f32_e32 v90, 0x43000000, v90
	v_mul_f32_e32 v91, 0x43000000, v91
	ds_write_b128 v5, v[88:91] offset:5120
	v_mul_f32_e32 v92, 0x43000000, v92
	v_mul_f32_e32 v93, 0x43000000, v93
	v_mul_f32_e32 v94, 0x43000000, v94
	v_mul_f32_e32 v95, 0x43000000, v95
	ds_write_b128 v5, v[92:95] offset:6144
	v_mul_f32_e32 v96, 0x43000000, v96
	v_mul_f32_e32 v97, 0x43000000, v97
	v_mul_f32_e32 v98, 0x43000000, v98
	v_mul_f32_e32 v99, 0x43000000, v99
	ds_write_b128 v5, v[96:99] offset:7168
	s_waitcnt lgkmcnt(0)
	s_barrier
; #define GAS __attribute__((address_space(1)))
; #define LAS __attribute__((address_space(3)))
; #define LDS_WAIT() asm volatile("s_waitcnt lgkmcnt(0)" ::: "memory")
; __device__ __forceinline__ unsigned pk4_fp8(float a, float b, float c, float d) {
;     a = fminf(fmaxf(a, -448.f), 448.f); b = fminf(fmaxf(b, -448.f), 448.f); c = fminf(fmaxf(c, -448.f), 448.f); d = fminf(fmaxf(d, -448.f), 448.f);
;     int w = __builtin_amdgcn_cvt_pk_fp8_f32(a, b, 0, false); w = __builtin_amdgcn_cvt_pk_fp8_f32(c, d, w, true); return (unsigned)w; }
;     const int pr = item >> 1, kb = 2 * (pr / nblk) + (item & 1), nb = pr % nblk, k0 = 64 * kb, n0 = 32 * nb;
;     const int nr = n0 + (lane & 31); const int sc = MAP == 1 ? src_col_in(nr) : nr;
;     float v[32];
; #pragma unroll
;     for (int i = 0; i < 32; ++i) v[i] = sc >= 0 ? W[(size_t)(k0 + 2 * i + (lane >> 5)) * Nsrc + sc] : 0.f;
; #pragma unroll
;     for (int i = 0; i < 32; ++i) { const int k = k0 + 2 * i + (lane >> 5); float x = v[i] * wscale; if (KS) x *= (k < ksplit ? ksA[k] : ksB[k - ksplit]); scr[(2 * i + (lane >> 5)) * 33 + (lane & 31)] = x; }
;     LDS_WAIT(); asm volatile("" ::: "memory");
;     const int c = lane & 7;
; #pragma unroll
;     for (int j = 0; j < 4; ++j) { const int n = (lane >> 3) + 8 * j; const LAS float* s = scr + (8 * c) * 33 + n;
;         const unsigned long long o = (unsigned long long)pg8::pk4_fp8(s[0 * 33], s[1 * 33], s[2 * 33], s[3 * 33]) | ((unsigned long long)pg8::pk4_fp8(s[4 * 33], s[5 * 33], s[6 * 33], s[7 * 33]) << 32);
;         *(GAS unsigned long long*)(WT + (size_t)(n0 + n) * K + k0 + 8 * c) = o; }
;     LDS_WAIT(); asm volatile("" ::: "memory");
; }
	s_add_i32 s17, s16, 1248
	s_min_u32 s17, s17, 0xfff
	s_lshr_b32 s18, s17, 5
	s_add_i32 s18, s18, 0
	s_and_b32 s19, s17, 31
	s_lshl_b32 s18, s18, 21
	s_lshl_b32 s19, s19, 9
	s_add_u32 s18, s18, s19
	s_add_u32 s12, s2, s18
	s_addc_u32 s13, s3, 0
	global_load_dwordx4 v[68:71], v10, s[12:13]
	s_add_u32 s12, s12, 0x8000
	s_addc_u32 s13, s13, 0
	global_load_dwordx4 v[72:75], v10, s[12:13]
	s_add_u32 s12, s12, 0x8000
	s_addc_u32 s13, s13, 0
	global_load_dwordx4 v[76:79], v10, s[12:13]
	s_add_u32 s12, s12, 0x8000
	s_addc_u32 s13, s13, 0
	global_load_dwordx4 v[80:83], v10, s[12:13]
	s_add_u32 s12, s12, 0x8000
	s_addc_u32 s13, s13, 0
	global_load_dwordx4 v[84:87], v10, s[12:13]
	s_add_u32 s12, s12, 0x8000
	s_addc_u32 s13, s13, 0
	global_load_dwordx4 v[88:91], v10, s[12:13]
	s_add_u32 s12, s12, 0x8000
	s_addc_u32 s13, s13, 0
	global_load_dwordx4 v[92:95], v10, s[12:13]
	s_add_u32 s12, s12, 0x8000
	s_addc_u32 s13, s13, 0
	global_load_dwordx4 v[96:99], v10, s[12:13]
	s_add_i32 s17, s16, 864
	s_min_u32 s17, s17, 0xfff
	s_lshr_b32 s18, s17, 5
	s_add_i32 s18, s18, 0
	s_and_b32 s19, s17, 31
	s_lshl_b32 s19, s19, 21
	s_lshl_b32 s18, s18, 7
	s_add_u32 s18, s18, s19
	s_add_u32 s14, s4, s18
	s_addc_u32 s15, s5, 0
	ds_read_b32 v170, v7
	ds_read_b32 v171, v7 offset:512
	ds_read_b32 v172, v7 offset:1024
	ds_read_b32 v173, v7 offset:1536
	ds_read_b32 v174, v7 offset:2048
	ds_read_b32 v175, v7 offset:2560
	ds_read_b32 v176, v7 offset:3072
	ds_read_b32 v177, v7 offset:3584
	ds_read_b32 v196, v7 offset:4096
	ds_read_b32 v197, v7 offset:4608
	ds_read_b32 v198, v7 offset:5120
	ds_read_b32 v199, v7 offset:5632
	ds_read_b32 v200, v7 offset:6144
	ds_read_b32 v201, v7 offset:6656
	ds_read_b32 v202, v7 offset:7168
	ds_read_b32 v203, v7 offset:7680
	s_waitcnt lgkmcnt(0)
	v_max_f32_e32 v170, v170, v170
	v_max_f32_e32 v171, v171, v171
	v_max_f32_e32 v172, v172, v172
	v_max_f32_e32 v173, v173, v173
	v_max_f32_e32 v174, v174, v174
	v_max_f32_e32 v175, v175, v175
	v_max_f32_e32 v176, v176, v176
	v_max_f32_e32 v177, v177, v177
	v_max_f32_e32 v196, v196, v196
	v_max_f32_e32 v197, v197, v197
	v_max_f32_e32 v198, v198, v198
	v_max_f32_e32 v199, v199, v199
	v_max_f32_e32 v200, v200, v200
	v_max_f32_e32 v201, v201, v201
	v_max_f32_e32 v202, v202, v202
	v_max_f32_e32 v203, v203, v203
	v_med3_f32 v170, v170, s20, v13
	v_med3_f32 v171, v171, s20, v13
	v_med3_f32 v172, v172, s20, v13
	v_med3_f32 v173, v173, s20, v13
	v_med3_f32 v174, v174, s20, v13
	v_med3_f32 v175, v175, s20, v13
	v_med3_f32 v176, v176, s20, v13
	v_med3_f32 v177, v177, s20, v13
	v_med3_f32 v196, v196, s20, v13
	v_med3_f32 v197, v197, s20, v13
	v_med3_f32 v198, v198, s20, v13
	v_med3_f32 v199, v199, s20, v13
	v_med3_f32 v200, v200, s20, v13
	v_med3_f32 v201, v201, s20, v13
	v_med3_f32 v202, v202, s20, v13
	v_med3_f32 v203, v203, s20, v13
	v_mov_b32_e32 v208, 0
	v_mov_b32_e32 v209, 0
	v_mov_b32_e32 v210, 0
	v_mov_b32_e32 v211, 0
	v_cvt_pk_fp8_f32 v208, v170, v171
	v_cvt_pk_fp8_f32 v209, v174, v175
	v_cvt_pk_fp8_f32 v210, v196, v197
	v_cvt_pk_fp8_f32 v211, v200, v201
	v_cvt_pk_fp8_f32 v208, v172, v173 op_sel:[0,0,1]
	v_cvt_pk_fp8_f32 v209, v176, v177 op_sel:[0,0,1]
	v_cvt_pk_fp8_f32 v210, v198, v199 op_sel:[0,0,1]
	v_cvt_pk_fp8_f32 v211, v202, v203 op_sel:[0,0,1]
	s_nop 0
	global_store_dwordx4 v11, v[208:211], s[14:15]
	ds_read_b32 v170, v9
	ds_read_b32 v171, v9 offset:512
	ds_read_b32 v172, v9 offset:1024
	ds_read_b32 v173, v9 offset:1536
	ds_read_b32 v174, v9 offset:2048
	ds_read_b32 v175, v9 offset:2560
	ds_read_b32 v176, v9 offset:3072
	ds_read_b32 v177, v9 offset:3584
	ds_read_b32 v196, v9 offset:4096
	ds_read_b32 v197, v9 offset:4608
	ds_read_b32 v198, v9 offset:5120
	ds_read_b32 v199, v9 offset:5632
	ds_read_b32 v200, v9 offset:6144
	ds_read_b32 v201, v9 offset:6656
	ds_read_b32 v202, v9 offset:7168
	ds_read_b32 v203, v9 offset:7680
	s_waitcnt lgkmcnt(0)
	v_max_f32_e32 v170, v170, v170
	v_max_f32_e32 v171, v171, v171
	v_max_f32_e32 v172, v172, v172
	v_max_f32_e32 v173, v173, v173
	v_max_f32_e32 v174, v174, v174
	v_max_f32_e32 v175, v175, v175
	v_max_f32_e32 v176, v176, v176
	v_max_f32_e32 v177, v177, v177
	v_max_f32_e32 v196, v196, v196
	v_max_f32_e32 v197, v197, v197
	v_max_f32_e32 v198, v198, v198
	v_max_f32_e32 v199, v199, v199
	v_max_f32_e32 v200, v200, v200
	v_max_f32_e32 v201, v201, v201
	v_max_f32_e32 v202, v202, v202
	v_max_f32_e32 v203, v203, v203
	v_med3_f32 v170, v170, s20, v13
	v_med3_f32 v171, v171, s20, v13
	v_med3_f32 v172, v172, s20, v13
	v_med3_f32 v173, v173, s20, v13
	v_med3_f32 v174, v174, s20, v13
	v_med3_f32 v175, v175, s20, v13
	v_med3_f32 v176, v176, s20, v13
	v_med3_f32 v177, v177, s20, v13
	v_med3_f32 v196, v196, s20, v13
	v_med3_f32 v197, v197, s20, v13
	v_med3_f32 v198, v198, s20, v13
	v_med3_f32 v199, v199, s20, v13
	v_med3_f32 v200, v200, s20, v13
	v_med3_f32 v201, v201, s20, v13
	v_med3_f32 v202, v202, s20, v13
	v_med3_f32 v203, v203, s20, v13
	v_mov_b32_e32 v208, 0
	v_mov_b32_e32 v209, 0
	v_mov_b32_e32 v210, 0
	v_mov_b32_e32 v211, 0
	v_cvt_pk_fp8_f32 v208, v170, v171
	v_cvt_pk_fp8_f32 v209, v174, v175
	v_cvt_pk_fp8_f32 v210, v196, v197
	v_cvt_pk_fp8_f32 v211, v200, v201
	v_cvt_pk_fp8_f32 v208, v172, v173 op_sel:[0,0,1]
	v_cvt_pk_fp8_f32 v209, v176, v177 op_sel:[0,0,1]
	v_cvt_pk_fp8_f32 v210, v198, v199 op_sel:[0,0,1]
	v_cvt_pk_fp8_f32 v211, v202, v203 op_sel:[0,0,1]
	s_nop 0
	global_store_dwordx4 v12, v[208:211], s[14:15]
	s_waitcnt vmcnt(32)
	v_mul_f32_e32 v100, 0x43000000, v100
	v_mul_f32_e32 v101, 0x43000000, v101
	v_mul_f32_e32 v102, 0x43000000, v102
	v_mul_f32_e32 v103, 0x43000000, v103
	ds_write_b128 v4, v[100:103]
	v_mul_f32_e32 v104, 0x43000000, v104
	v_mul_f32_e32 v105, 0x43000000, v105
	v_mul_f32_e32 v106, 0x43000000, v106
	v_mul_f32_e32 v107, 0x43000000, v107
	ds_write_b128 v4, v[104:107] offset:1024
	v_mul_f32_e32 v108, 0x43000000, v108
	v_mul_f32_e32 v109, 0x43000000, v109
	v_mul_f32_e32 v110, 0x43000000, v110
	v_mul_f32_e32 v111, 0x43000000, v111
	ds_write_b128 v4, v[108:111] offset:2048
	v_mul_f32_e32 v112, 0x43000000, v112
	v_mul_f32_e32 v113, 0x43000000, v113
	v_mul_f32_e32 v114, 0x43000000, v114
	v_mul_f32_e32 v115, 0x43000000, v115
	ds_write_b128 v4, v[112:115] offset:3072
	v_mul_f32_e32 v116, 0x43000000, v116
	v_mul_f32_e32 v117, 0x43000000, v117
	v_mul_f32_e32 v118, 0x43000000, v118
	v_mul_f32_e32 v119, 0x43000000, v119
	ds_write_b128 v4, v[116:119] offset:4096
	v_mul_f32_e32 v120, 0x43000000, v120
	v_mul_f32_e32 v121, 0x43000000, v121
	v_mul_f32_e32 v122, 0x43000000, v122
	v_mul_f32_e32 v123, 0x43000000, v123
	ds_write_b128 v4, v[120:123] offset:5120
	v_mul_f32_e32 v124, 0x43000000, v124
	v_mul_f32_e32 v125, 0x43000000, v125
	v_mul_f32_e32 v126, 0x43000000, v126
	v_mul_f32_e32 v127, 0x43000000, v127
	ds_write_b128 v4, v[124:127] offset:6144
	v_mul_f32_e32 v128, 0x43000000, v128
	v_mul_f32_e32 v129, 0x43000000, v129
	v_mul_f32_e32 v130, 0x43000000, v130
	v_mul_f32_e32 v131, 0x43000000, v131
	ds_write_b128 v4, v[128:131] offset:7168
	s_waitcnt lgkmcnt(0)
	s_barrier
; #define GAS __attribute__((address_space(1)))
; #define LAS __attribute__((address_space(3)))
; #define LDS_WAIT() asm volatile("s_waitcnt lgkmcnt(0)" ::: "memory")
; __device__ __forceinline__ unsigned pk4_fp8(float a, float b, float c, float d) {
;     a = fminf(fmaxf(a, -448.f), 448.f); b = fminf(fmaxf(b, -448.f), 448.f); c = fminf(fmaxf(c, -448.f), 448.f); d = fminf(fmaxf(d, -448.f), 448.f);
;     int w = __builtin_amdgcn_cvt_pk_fp8_f32(a, b, 0, false); w = __builtin_amdgcn_cvt_pk_fp8_f32(c, d, w, true); return (unsigned)w; }
;     const int pr = item >> 1, kb = 2 * (pr / nblk) + (item & 1), nb = pr % nblk, k0 = 64 * kb, n0 = 32 * nb;
;     const int nr = n0 + (lane & 31); const int sc = MAP == 1 ? src_col_in(nr) : nr;
;     float v[32];
; #pragma unroll
;     for (int i = 0; i < 32; ++i) v[i] = sc >= 0 ? W[(size_t)(k0 + 2 * i + (lane >> 5)) * Nsrc + sc] : 0.f;
; #pragma unroll
;     for (int i = 0; i < 32; ++i) { const int k = k0 + 2 * i + (lane >> 5); float x = v[i] * wscale; if (KS) x *= (k < ksplit ? ksA[k] : ksB[k - ksplit]); scr[(2 * i + (lane >> 5)) * 33 + (lane & 31)] = x; }
;     LDS_WAIT(); asm volatile("" ::: "memory");
;     const int c = lane & 7;
; #pragma unroll
;     for (int j = 0; j < 4; ++j) { const int n = (lane >> 3) + 8 * j; const LAS float* s = scr + (8 * c) * 33 + n;
;         const unsigned long long o = (unsigned long long)pg8::pk4_fp8(s[0 * 33], s[1 * 33], s[2 * 33], s[3 * 33]) | ((unsigned long long)pg8::pk4_fp8(s[4 * 33], s[5 * 33], s[6 * 33], s[7 * 33]) << 32);
;         *(GAS unsigned long long*)(WT + (size_t)(n0 + n) * K + k0 + 8 * c) = o; }
;     LDS_WAIT(); asm volatile("" ::: "memory");
; }
	s_add_i32 s17, s16, 1344
	s_min_u32 s17, s17, 0xfff
	s_lshr_b32 s18, s17, 5
	s_add_i32 s18, s18, 0
	s_and_b32 s19, s17, 31
	s_lshl_b32 s18, s18, 21
	s_lshl_b32 s19, s19, 9
	s_add_u32 s18, s18, s19
	s_add_u32 s12, s2, s18
	s_addc_u32 s13, s3, 0
	global_load_dwordx4 v[100:103], v10, s[12:13]
	s_add_u32 s12, s12, 0x8000
	s_addc_u32 s13, s13, 0
	global_load_dwordx4 v[104:107], v10, s[12:13]
	s_add_u32 s12, s12, 0x8000
	s_addc_u32 s13, s13, 0
	global_load_dwordx4 v[108:111], v10, s[12:13]
	s_add_u32 s12, s12, 0x8000
	s_addc_u32 s13, s13, 0
	global_load_dwordx4 v[112:115], v10, s[12:13]
	s_add_u32 s12, s12, 0x8000
	s_addc_u32 s13, s13, 0
	global_load_dwordx4 v[116:119], v10, s[12:13]
	s_add_u32 s12, s12, 0x8000
	s_addc_u32 s13, s13, 0
	global_load_dwordx4 v[120:123], v10, s[12:13]
	s_add_u32 s12, s12, 0x8000
	s_addc_u32 s13, s13, 0
	global_load_dwordx4 v[124:127], v10, s[12:13]
	s_add_u32 s12, s12, 0x8000
	s_addc_u32 s13, s13, 0
	global_load_dwordx4 v[128:131], v10, s[12:13]
	s_add_i32 s17, s16, 960
	s_min_u32 s17, s17, 0xfff
	s_lshr_b32 s18, s17, 5
	s_add_i32 s18, s18, 0
	s_and_b32 s19, s17, 31
	s_lshl_b32 s19, s19, 21
	s_lshl_b32 s18, s18, 7
	s_add_u32 s18, s18, s19
	s_add_u32 s14, s4, s18
	s_addc_u32 s15, s5, 0
	ds_read_b32 v170, v6
	ds_read_b32 v171, v6 offset:512
	ds_read_b32 v172, v6 offset:1024
	ds_read_b32 v173, v6 offset:1536
	ds_read_b32 v174, v6 offset:2048
	ds_read_b32 v175, v6 offset:2560
	ds_read_b32 v176, v6 offset:3072
	ds_read_b32 v177, v6 offset:3584
	ds_read_b32 v196, v6 offset:4096
	ds_read_b32 v197, v6 offset:4608
	ds_read_b32 v198, v6 offset:5120
	ds_read_b32 v199, v6 offset:5632
	ds_read_b32 v200, v6 offset:6144
	ds_read_b32 v201, v6 offset:6656
	ds_read_b32 v202, v6 offset:7168
	ds_read_b32 v203, v6 offset:7680
	s_waitcnt lgkmcnt(0)
	v_max_f32_e32 v170, v170, v170
	v_max_f32_e32 v171, v171, v171
	v_max_f32_e32 v172, v172, v172
	v_max_f32_e32 v173, v173, v173
	v_max_f32_e32 v174, v174, v174
	v_max_f32_e32 v175, v175, v175
	v_max_f32_e32 v176, v176, v176
	v_max_f32_e32 v177, v177, v177
	v_max_f32_e32 v196, v196, v196
	v_max_f32_e32 v197, v197, v197
	v_max_f32_e32 v198, v198, v198
	v_max_f32_e32 v199, v199, v199
	v_max_f32_e32 v200, v200, v200
	v_max_f32_e32 v201, v201, v201
	v_max_f32_e32 v202, v202, v202
	v_max_f32_e32 v203, v203, v203
	v_med3_f32 v170, v170, s20, v13
	v_med3_f32 v171, v171, s20, v13
	v_med3_f32 v172, v172, s20, v13
	v_med3_f32 v173, v173, s20, v13
	v_med3_f32 v174, v174, s20, v13
	v_med3_f32 v175, v175, s20, v13
	v_med3_f32 v176, v176, s20, v13
	v_med3_f32 v177, v177, s20, v13
	v_med3_f32 v196, v196, s20, v13
	v_med3_f32 v197, v197, s20, v13
	v_med3_f32 v198, v198, s20, v13
	v_med3_f32 v199, v199, s20, v13
	v_med3_f32 v200, v200, s20, v13
	v_med3_f32 v201, v201, s20, v13
	v_med3_f32 v202, v202, s20, v13
	v_med3_f32 v203, v203, s20, v13
	v_mov_b32_e32 v208, 0
	v_mov_b32_e32 v209, 0
	v_mov_b32_e32 v210, 0
	v_mov_b32_e32 v211, 0
	v_cvt_pk_fp8_f32 v208, v170, v171
	v_cvt_pk_fp8_f32 v209, v174, v175
	v_cvt_pk_fp8_f32 v210, v196, v197
	v_cvt_pk_fp8_f32 v211, v200, v201
	v_cvt_pk_fp8_f32 v208, v172, v173 op_sel:[0,0,1]
	v_cvt_pk_fp8_f32 v209, v176, v177 op_sel:[0,0,1]
	v_cvt_pk_fp8_f32 v210, v198, v199 op_sel:[0,0,1]
	v_cvt_pk_fp8_f32 v211, v202, v203 op_sel:[0,0,1]
	s_nop 0
	global_store_dwordx4 v11, v[208:211], s[14:15]
	ds_read_b32 v170, v8
	ds_read_b32 v171, v8 offset:512
	ds_read_b32 v172, v8 offset:1024
	ds_read_b32 v173, v8 offset:1536
	ds_read_b32 v174, v8 offset:2048
	ds_read_b32 v175, v8 offset:2560
	ds_read_b32 v176, v8 offset:3072
	ds_read_b32 v177, v8 offset:3584
	ds_read_b32 v196, v8 offset:4096
	ds_read_b32 v197, v8 offset:4608
	ds_read_b32 v198, v8 offset:5120
	ds_read_b32 v199, v8 offset:5632
	ds_read_b32 v200, v8 offset:6144
	ds_read_b32 v201, v8 offset:6656
	ds_read_b32 v202, v8 offset:7168
	ds_read_b32 v203, v8 offset:7680
	s_waitcnt lgkmcnt(0)
	v_max_f32_e32 v170, v170, v170
	v_max_f32_e32 v171, v171, v171
	v_max_f32_e32 v172, v172, v172
	v_max_f32_e32 v173, v173, v173
	v_max_f32_e32 v174, v174, v174
	v_max_f32_e32 v175, v175, v175
	v_max_f32_e32 v176, v176, v176
	v_max_f32_e32 v177, v177, v177
	v_max_f32_e32 v196, v196, v196
	v_max_f32_e32 v197, v197, v197
	v_max_f32_e32 v198, v198, v198
	v_max_f32_e32 v199, v199, v199
	v_max_f32_e32 v200, v200, v200
	v_max_f32_e32 v201, v201, v201
	v_max_f32_e32 v202, v202, v202
	v_max_f32_e32 v203, v203, v203
	v_med3_f32 v170, v170, s20, v13
	v_med3_f32 v171, v171, s20, v13
	v_med3_f32 v172, v172, s20, v13
	v_med3_f32 v173, v173, s20, v13
	v_med3_f32 v174, v174, s20, v13
	v_med3_f32 v175, v175, s20, v13
	v_med3_f32 v176, v176, s20, v13
	v_med3_f32 v177, v177, s20, v13
	v_med3_f32 v196, v196, s20, v13
	v_med3_f32 v197, v197, s20, v13
	v_med3_f32 v198, v198, s20, v13
	v_med3_f32 v199, v199, s20, v13
	v_med3_f32 v200, v200, s20, v13
	v_med3_f32 v201, v201, s20, v13
	v_med3_f32 v202, v202, s20, v13
	v_med3_f32 v203, v203, s20, v13
	v_mov_b32_e32 v208, 0
	v_mov_b32_e32 v209, 0
	v_mov_b32_e32 v210, 0
	v_mov_b32_e32 v211, 0
	v_cvt_pk_fp8_f32 v208, v170, v171
	v_cvt_pk_fp8_f32 v209, v174, v175
	v_cvt_pk_fp8_f32 v210, v196, v197
	v_cvt_pk_fp8_f32 v211, v200, v201
	v_cvt_pk_fp8_f32 v208, v172, v173 op_sel:[0,0,1]
	v_cvt_pk_fp8_f32 v209, v176, v177 op_sel:[0,0,1]
	v_cvt_pk_fp8_f32 v210, v198, v199 op_sel:[0,0,1]
	v_cvt_pk_fp8_f32 v211, v202, v203 op_sel:[0,0,1]
	s_nop 0
	global_store_dwordx4 v12, v[208:211], s[14:15]
	s_waitcnt vmcnt(32)
	v_mul_f32_e32 v132, 0x43000000, v132
	v_mul_f32_e32 v133, 0x43000000, v133
	v_mul_f32_e32 v134, 0x43000000, v134
	v_mul_f32_e32 v135, 0x43000000, v135
	ds_write_b128 v5, v[132:135]
	v_mul_f32_e32 v136, 0x43000000, v136
	v_mul_f32_e32 v137, 0x43000000, v137
	v_mul_f32_e32 v138, 0x43000000, v138
	v_mul_f32_e32 v139, 0x43000000, v139
	ds_write_b128 v5, v[136:139] offset:1024
	v_mul_f32_e32 v140, 0x43000000, v140
	v_mul_f32_e32 v141, 0x43000000, v141
	v_mul_f32_e32 v142, 0x43000000, v142
	v_mul_f32_e32 v143, 0x43000000, v143
	ds_write_b128 v5, v[140:143] offset:2048
	v_mul_f32_e32 v144, 0x43000000, v144
	v_mul_f32_e32 v145, 0x43000000, v145
	v_mul_f32_e32 v146, 0x43000000, v146
	v_mul_f32_e32 v147, 0x43000000, v147
	ds_write_b128 v5, v[144:147] offset:3072
	v_mul_f32_e32 v148, 0x43000000, v148
	v_mul_f32_e32 v149, 0x43000000, v149
	v_mul_f32_e32 v150, 0x43000000, v150
	v_mul_f32_e32 v151, 0x43000000, v151
	ds_write_b128 v5, v[148:151] offset:4096
	v_mul_f32_e32 v152, 0x43000000, v152
	v_mul_f32_e32 v153, 0x43000000, v153
	v_mul_f32_e32 v154, 0x43000000, v154
	v_mul_f32_e32 v155, 0x43000000, v155
	ds_write_b128 v5, v[152:155] offset:5120
	v_mul_f32_e32 v156, 0x43000000, v156
	v_mul_f32_e32 v157, 0x43000000, v157
	v_mul_f32_e32 v158, 0x43000000, v158
	v_mul_f32_e32 v159, 0x43000000, v159
	ds_write_b128 v5, v[156:159] offset:6144
	v_mul_f32_e32 v160, 0x43000000, v160
	v_mul_f32_e32 v161, 0x43000000, v161
	v_mul_f32_e32 v162, 0x43000000, v162
	v_mul_f32_e32 v163, 0x43000000, v163
	ds_write_b128 v5, v[160:163] offset:7168
	s_waitcnt lgkmcnt(0)
	s_barrier
; #define GAS __attribute__((address_space(1)))
; #define LAS __attribute__((address_space(3)))
; #define LDS_WAIT() asm volatile("s_waitcnt lgkmcnt(0)" ::: "memory")
; __device__ __forceinline__ unsigned pk4_fp8(float a, float b, float c, float d) {
;     a = fminf(fmaxf(a, -448.f), 448.f); b = fminf(fmaxf(b, -448.f), 448.f); c = fminf(fmaxf(c, -448.f), 448.f); d = fminf(fmaxf(d, -448.f), 448.f);
;     int w = __builtin_amdgcn_cvt_pk_fp8_f32(a, b, 0, false); w = __builtin_amdgcn_cvt_pk_fp8_f32(c, d, w, true); return (unsigned)w; }
;     const int pr = item >> 1, kb = 2 * (pr / nblk) + (item & 1), nb = pr % nblk, k0 = 64 * kb, n0 = 32 * nb;
;     const int nr = n0 + (lane & 31); const int sc = MAP == 1 ? src_col_in(nr) : nr;
;     float v[32];
; #pragma unroll
;     for (int i = 0; i < 32; ++i) v[i] = sc >= 0 ? W[(size_t)(k0 + 2 * i + (lane >> 5)) * Nsrc + sc] : 0.f;
; #pragma unroll
;     for (int i = 0; i < 32; ++i) { const int k = k0 + 2 * i + (lane >> 5); float x = v[i] * wscale; if (KS) x *= (k < ksplit ? ksA[k] : ksB[k - ksplit]); scr[(2 * i + (lane >> 5)) * 33 + (lane & 31)] = x; }
;     LDS_WAIT(); asm volatile("" ::: "memory");
;     const int c = lane & 7;
; #pragma unroll
;     for (int j = 0; j < 4; ++j) { const int n = (lane >> 3) + 8 * j; const LAS float* s = scr + (8 * c) * 33 + n;
;         const unsigned long long o = (unsigned long long)pg8::pk4_fp8(s[0 * 33], s[1 * 33], s[2 * 33], s[3 * 33]) | ((unsigned long long)pg8::pk4_fp8(s[4 * 33], s[5 * 33], s[6 * 33], s[7 * 33]) << 32);
;         *(GAS unsigned long long*)(WT + (size_t)(n0 + n) * K + k0 + 8 * c) = o; }
;     LDS_WAIT(); asm volatile("" ::: "memory");
; }
	s_add_i32 s17, s16, 1440
	s_min_u32 s17, s17, 0xfff
	s_lshr_b32 s18, s17, 5
	s_add_i32 s18, s18, 0
	s_and_b32 s19, s17, 31
	s_lshl_b32 s18, s18, 21
	s_lshl_b32 s19, s19, 9
	s_add_u32 s18, s18, s19
	s_add_u32 s12, s2, s18
	s_addc_u32 s13, s3, 0
	global_load_dwordx4 v[132:135], v10, s[12:13]
	s_add_u32 s12, s12, 0x8000
	s_addc_u32 s13, s13, 0
	global_load_dwordx4 v[136:139], v10, s[12:13]
	s_add_u32 s12, s12, 0x8000
	s_addc_u32 s13, s13, 0
	global_load_dwordx4 v[140:143], v10, s[12:13]
	s_add_u32 s12, s12, 0x8000
	s_addc_u32 s13, s13, 0
	global_load_dwordx4 v[144:147], v10, s[12:13]
	s_add_u32 s12, s12, 0x8000
	s_addc_u32 s13, s13, 0
	global_load_dwordx4 v[148:151], v10, s[12:13]
	s_add_u32 s12, s12, 0x8000
	s_addc_u32 s13, s13, 0
	global_load_dwordx4 v[152:155], v10, s[12:13]
	s_add_u32 s12, s12, 0x8000
	s_addc_u32 s13, s13, 0
	global_load_dwordx4 v[156:159], v10, s[12:13]
	s_add_u32 s12, s12, 0x8000
	s_addc_u32 s13, s13, 0
	global_load_dwordx4 v[160:163], v10, s[12:13]
	s_add_i32 s17, s16, 1056
	s_min_u32 s17, s17, 0xfff
	s_lshr_b32 s18, s17, 5
	s_add_i32 s18, s18, 0
	s_and_b32 s19, s17, 31
	s_lshl_b32 s19, s19, 21
	s_lshl_b32 s18, s18, 7
	s_add_u32 s18, s18, s19
	s_add_u32 s14, s4, s18
	s_addc_u32 s15, s5, 0
	ds_read_b32 v170, v7
	ds_read_b32 v171, v7 offset:512
	ds_read_b32 v172, v7 offset:1024
	ds_read_b32 v173, v7 offset:1536
	ds_read_b32 v174, v7 offset:2048
	ds_read_b32 v175, v7 offset:2560
	ds_read_b32 v176, v7 offset:3072
	ds_read_b32 v177, v7 offset:3584
	ds_read_b32 v196, v7 offset:4096
	ds_read_b32 v197, v7 offset:4608
	ds_read_b32 v198, v7 offset:5120
	ds_read_b32 v199, v7 offset:5632
	ds_read_b32 v200, v7 offset:6144
	ds_read_b32 v201, v7 offset:6656
	ds_read_b32 v202, v7 offset:7168
	ds_read_b32 v203, v7 offset:7680
	s_waitcnt lgkmcnt(0)
	v_max_f32_e32 v170, v170, v170
	v_max_f32_e32 v171, v171, v171
	v_max_f32_e32 v172, v172, v172
	v_max_f32_e32 v173, v173, v173
	v_max_f32_e32 v174, v174, v174
	v_max_f32_e32 v175, v175, v175
	v_max_f32_e32 v176, v176, v176
	v_max_f32_e32 v177, v177, v177
	v_max_f32_e32 v196, v196, v196
	v_max_f32_e32 v197, v197, v197
	v_max_f32_e32 v198, v198, v198
	v_max_f32_e32 v199, v199, v199
	v_max_f32_e32 v200, v200, v200
	v_max_f32_e32 v201, v201, v201
	v_max_f32_e32 v202, v202, v202
	v_max_f32_e32 v203, v203, v203
	v_med3_f32 v170, v170, s20, v13
	v_med3_f32 v171, v171, s20, v13
	v_med3_f32 v172, v172, s20, v13
	v_med3_f32 v173, v173, s20, v13
	v_med3_f32 v174, v174, s20, v13
	v_med3_f32 v175, v175, s20, v13
	v_med3_f32 v176, v176, s20, v13
	v_med3_f32 v177, v177, s20, v13
	v_med3_f32 v196, v196, s20, v13
	v_med3_f32 v197, v197, s20, v13
	v_med3_f32 v198, v198, s20, v13
	v_med3_f32 v199, v199, s20, v13
	v_med3_f32 v200, v200, s20, v13
	v_med3_f32 v201, v201, s20, v13
	v_med3_f32 v202, v202, s20, v13
	v_med3_f32 v203, v203, s20, v13
	v_mov_b32_e32 v208, 0
	v_mov_b32_e32 v209, 0
	v_mov_b32_e32 v210, 0
	v_mov_b32_e32 v211, 0
	v_cvt_pk_fp8_f32 v208, v170, v171
	v_cvt_pk_fp8_f32 v209, v174, v175
	v_cvt_pk_fp8_f32 v210, v196, v197
	v_cvt_pk_fp8_f32 v211, v200, v201
	v_cvt_pk_fp8_f32 v208, v172, v173 op_sel:[0,0,1]
	v_cvt_pk_fp8_f32 v209, v176, v177 op_sel:[0,0,1]
	v_cvt_pk_fp8_f32 v210, v198, v199 op_sel:[0,0,1]
	v_cvt_pk_fp8_f32 v211, v202, v203 op_sel:[0,0,1]
	s_nop 0
	global_store_dwordx4 v11, v[208:211], s[14:15]
	ds_read_b32 v170, v9
	ds_read_b32 v171, v9 offset:512
	ds_read_b32 v172, v9 offset:1024
	ds_read_b32 v173, v9 offset:1536
	ds_read_b32 v174, v9 offset:2048
	ds_read_b32 v175, v9 offset:2560
	ds_read_b32 v176, v9 offset:3072
	ds_read_b32 v177, v9 offset:3584
	ds_read_b32 v196, v9 offset:4096
	ds_read_b32 v197, v9 offset:4608
	ds_read_b32 v198, v9 offset:5120
	ds_read_b32 v199, v9 offset:5632
	ds_read_b32 v200, v9 offset:6144
	ds_read_b32 v201, v9 offset:6656
	ds_read_b32 v202, v9 offset:7168
	ds_read_b32 v203, v9 offset:7680
	s_waitcnt lgkmcnt(0)
	v_max_f32_e32 v170, v170, v170
	v_max_f32_e32 v171, v171, v171
	v_max_f32_e32 v172, v172, v172
	v_max_f32_e32 v173, v173, v173
	v_max_f32_e32 v174, v174, v174
	v_max_f32_e32 v175, v175, v175
	v_max_f32_e32 v176, v176, v176
	v_max_f32_e32 v177, v177, v177
	v_max_f32_e32 v196, v196, v196
	v_max_f32_e32 v197, v197, v197
	v_max_f32_e32 v198, v198, v198
	v_max_f32_e32 v199, v199, v199
	v_max_f32_e32 v200, v200, v200
	v_max_f32_e32 v201, v201, v201
	v_max_f32_e32 v202, v202, v202
	v_max_f32_e32 v203, v203, v203
	v_med3_f32 v170, v170, s20, v13
	v_med3_f32 v171, v171, s20, v13
	v_med3_f32 v172, v172, s20, v13
	v_med3_f32 v173, v173, s20, v13
	v_med3_f32 v174, v174, s20, v13
	v_med3_f32 v175, v175, s20, v13
	v_med3_f32 v176, v176, s20, v13
	v_med3_f32 v177, v177, s20, v13
	v_med3_f32 v196, v196, s20, v13
	v_med3_f32 v197, v197, s20, v13
	v_med3_f32 v198, v198, s20, v13
	v_med3_f32 v199, v199, s20, v13
	v_med3_f32 v200, v200, s20, v13
	v_med3_f32 v201, v201, s20, v13
	v_med3_f32 v202, v202, s20, v13
	v_med3_f32 v203, v203, s20, v13
	v_mov_b32_e32 v208, 0
	v_mov_b32_e32 v209, 0
	v_mov_b32_e32 v210, 0
	v_mov_b32_e32 v211, 0
	v_cvt_pk_fp8_f32 v208, v170, v171
	v_cvt_pk_fp8_f32 v209, v174, v175
	v_cvt_pk_fp8_f32 v210, v196, v197
	v_cvt_pk_fp8_f32 v211, v200, v201
	v_cvt_pk_fp8_f32 v208, v172, v173 op_sel:[0,0,1]
	v_cvt_pk_fp8_f32 v209, v176, v177 op_sel:[0,0,1]
	v_cvt_pk_fp8_f32 v210, v198, v199 op_sel:[0,0,1]
	v_cvt_pk_fp8_f32 v211, v202, v203 op_sel:[0,0,1]
	s_nop 0
	global_store_dwordx4 v12, v[208:211], s[14:15]
	s_waitcnt vmcnt(32)
	v_mul_f32_e32 v36, 0x43000000, v36
	v_mul_f32_e32 v37, 0x43000000, v37
	v_mul_f32_e32 v38, 0x43000000, v38
	v_mul_f32_e32 v39, 0x43000000, v39
	ds_write_b128 v4, v[36:39]
	v_mul_f32_e32 v40, 0x43000000, v40
	v_mul_f32_e32 v41, 0x43000000, v41
	v_mul_f32_e32 v42, 0x43000000, v42
	v_mul_f32_e32 v43, 0x43000000, v43
	ds_write_b128 v4, v[40:43] offset:1024
	v_mul_f32_e32 v44, 0x43000000, v44
	v_mul_f32_e32 v45, 0x43000000, v45
	v_mul_f32_e32 v46, 0x43000000, v46
	v_mul_f32_e32 v47, 0x43000000, v47
	ds_write_b128 v4, v[44:47] offset:2048
	v_mul_f32_e32 v48, 0x43000000, v48
	v_mul_f32_e32 v49, 0x43000000, v49
	v_mul_f32_e32 v50, 0x43000000, v50
	v_mul_f32_e32 v51, 0x43000000, v51
	ds_write_b128 v4, v[48:51] offset:3072
	v_mul_f32_e32 v52, 0x43000000, v52
	v_mul_f32_e32 v53, 0x43000000, v53
	v_mul_f32_e32 v54, 0x43000000, v54
	v_mul_f32_e32 v55, 0x43000000, v55
	ds_write_b128 v4, v[52:55] offset:4096
	v_mul_f32_e32 v56, 0x43000000, v56
	v_mul_f32_e32 v57, 0x43000000, v57
	v_mul_f32_e32 v58, 0x43000000, v58
	v_mul_f32_e32 v59, 0x43000000, v59
	ds_write_b128 v4, v[56:59] offset:5120
	v_mul_f32_e32 v60, 0x43000000, v60
	v_mul_f32_e32 v61, 0x43000000, v61
	v_mul_f32_e32 v62, 0x43000000, v62
	v_mul_f32_e32 v63, 0x43000000, v63
	ds_write_b128 v4, v[60:63] offset:6144
	v_mul_f32_e32 v64, 0x43000000, v64
	v_mul_f32_e32 v65, 0x43000000, v65
	v_mul_f32_e32 v66, 0x43000000, v66
	v_mul_f32_e32 v67, 0x43000000, v67
	ds_write_b128 v4, v[64:67] offset:7168
	s_waitcnt lgkmcnt(0)
	s_barrier
; #define GAS __attribute__((address_space(1)))
; #define LAS __attribute__((address_space(3)))
; #define LDS_WAIT() asm volatile("s_waitcnt lgkmcnt(0)" ::: "memory")
; __device__ __forceinline__ unsigned pk4_fp8(float a, float b, float c, float d) {
;     a = fminf(fmaxf(a, -448.f), 448.f); b = fminf(fmaxf(b, -448.f), 448.f); c = fminf(fmaxf(c, -448.f), 448.f); d = fminf(fmaxf(d, -448.f), 448.f);
;     int w = __builtin_amdgcn_cvt_pk_fp8_f32(a, b, 0, false); w = __builtin_amdgcn_cvt_pk_fp8_f32(c, d, w, true); return (unsigned)w; }
;     const int pr = item >> 1, kb = 2 * (pr / nblk) + (item & 1), nb = pr % nblk, k0 = 64 * kb, n0 = 32 * nb;
;     const int nr = n0 + (lane & 31); const int sc = MAP == 1 ? src_col_in(nr) : nr;
;     float v[32];
; #pragma unroll
;     for (int i = 0; i < 32; ++i) v[i] = sc >= 0 ? W[(size_t)(k0 + 2 * i + (lane >> 5)) * Nsrc + sc] : 0.f;
; #pragma unroll
;     for (int i = 0; i < 32; ++i) { const int k = k0 + 2 * i + (lane >> 5); float x = v[i] * wscale; if (KS) x *= (k < ksplit ? ksA[k] : ksB[k - ksplit]); scr[(2 * i + (lane >> 5)) * 33 + (lane & 31)] = x; }
;     LDS_WAIT(); asm volatile("" ::: "memory");
;     const int c = lane & 7;
; #pragma unroll
;     for (int j = 0; j < 4; ++j) { const int n = (lane >> 3) + 8 * j; const LAS float* s = scr + (8 * c) * 33 + n;
;         const unsigned long long o = (unsigned long long)pg8::pk4_fp8(s[0 * 33], s[1 * 33], s[2 * 33], s[3 * 33]) | ((unsigned long long)pg8::pk4_fp8(s[4 * 33], s[5 * 33], s[6 * 33], s[7 * 33]) << 32);
;         *(GAS unsigned long long*)(WT + (size_t)(n0 + n) * K + k0 + 8 * c) = o; }
;     LDS_WAIT(); asm volatile("" ::: "memory");
; }
	s_add_i32 s17, s16, 1536
	s_min_u32 s17, s17, 0xfff
	s_lshr_b32 s18, s17, 5
	s_add_i32 s18, s18, 0
	s_and_b32 s19, s17, 31
	s_lshl_b32 s18, s18, 21
	s_lshl_b32 s19, s19, 9
	s_add_u32 s18, s18, s19
	s_add_u32 s12, s2, s18
	s_addc_u32 s13, s3, 0
	global_load_dwordx4 v[36:39], v10, s[12:13]
	s_add_u32 s12, s12, 0x8000
	s_addc_u32 s13, s13, 0
	global_load_dwordx4 v[40:43], v10, s[12:13]
	s_add_u32 s12, s12, 0x8000
	s_addc_u32 s13, s13, 0
	global_load_dwordx4 v[44:47], v10, s[12:13]
	s_add_u32 s12, s12, 0x8000
	s_addc_u32 s13, s13, 0
	global_load_dwordx4 v[48:51], v10, s[12:13]
	s_add_u32 s12, s12, 0x8000
	s_addc_u32 s13, s13, 0
	global_load_dwordx4 v[52:55], v10, s[12:13]
	s_add_u32 s12, s12, 0x8000
	s_addc_u32 s13, s13, 0
	global_load_dwordx4 v[56:59], v10, s[12:13]
	s_add_u32 s12, s12, 0x8000
	s_addc_u32 s13, s13, 0
	global_load_dwordx4 v[60:63], v10, s[12:13]
	s_add_u32 s12, s12, 0x8000
	s_addc_u32 s13, s13, 0
	global_load_dwordx4 v[64:67], v10, s[12:13]
	s_add_i32 s17, s16, 1152
	s_min_u32 s17, s17, 0xfff
	s_lshr_b32 s18, s17, 5
	s_add_i32 s18, s18, 0
	s_and_b32 s19, s17, 31
	s_lshl_b32 s19, s19, 21
	s_lshl_b32 s18, s18, 7
	s_add_u32 s18, s18, s19
	s_add_u32 s14, s4, s18
	s_addc_u32 s15, s5, 0
	ds_read_b32 v170, v6
	ds_read_b32 v171, v6 offset:512
	ds_read_b32 v172, v6 offset:1024
	ds_read_b32 v173, v6 offset:1536
	ds_read_b32 v174, v6 offset:2048
	ds_read_b32 v175, v6 offset:2560
	ds_read_b32 v176, v6 offset:3072
	ds_read_b32 v177, v6 offset:3584
	ds_read_b32 v196, v6 offset:4096
	ds_read_b32 v197, v6 offset:4608
	ds_read_b32 v198, v6 offset:5120
	ds_read_b32 v199, v6 offset:5632
	ds_read_b32 v200, v6 offset:6144
	ds_read_b32 v201, v6 offset:6656
	ds_read_b32 v202, v6 offset:7168
	ds_read_b32 v203, v6 offset:7680
	s_waitcnt lgkmcnt(0)
	v_max_f32_e32 v170, v170, v170
	v_max_f32_e32 v171, v171, v171
	v_max_f32_e32 v172, v172, v172
	v_max_f32_e32 v173, v173, v173
	v_max_f32_e32 v174, v174, v174
	v_max_f32_e32 v175, v175, v175
	v_max_f32_e32 v176, v176, v176
	v_max_f32_e32 v177, v177, v177
	v_max_f32_e32 v196, v196, v196
	v_max_f32_e32 v197, v197, v197
	v_max_f32_e32 v198, v198, v198
	v_max_f32_e32 v199, v199, v199
	v_max_f32_e32 v200, v200, v200
	v_max_f32_e32 v201, v201, v201
	v_max_f32_e32 v202, v202, v202
	v_max_f32_e32 v203, v203, v203
	v_med3_f32 v170, v170, s20, v13
	v_med3_f32 v171, v171, s20, v13
	v_med3_f32 v172, v172, s20, v13
	v_med3_f32 v173, v173, s20, v13
	v_med3_f32 v174, v174, s20, v13
	v_med3_f32 v175, v175, s20, v13
	v_med3_f32 v176, v176, s20, v13
	v_med3_f32 v177, v177, s20, v13
	v_med3_f32 v196, v196, s20, v13
	v_med3_f32 v197, v197, s20, v13
	v_med3_f32 v198, v198, s20, v13
	v_med3_f32 v199, v199, s20, v13
	v_med3_f32 v200, v200, s20, v13
	v_med3_f32 v201, v201, s20, v13
	v_med3_f32 v202, v202, s20, v13
	v_med3_f32 v203, v203, s20, v13
	v_mov_b32_e32 v208, 0
	v_mov_b32_e32 v209, 0
	v_mov_b32_e32 v210, 0
	v_mov_b32_e32 v211, 0
	v_cvt_pk_fp8_f32 v208, v170, v171
	v_cvt_pk_fp8_f32 v209, v174, v175
	v_cvt_pk_fp8_f32 v210, v196, v197
	v_cvt_pk_fp8_f32 v211, v200, v201
	v_cvt_pk_fp8_f32 v208, v172, v173 op_sel:[0,0,1]
	v_cvt_pk_fp8_f32 v209, v176, v177 op_sel:[0,0,1]
	v_cvt_pk_fp8_f32 v210, v198, v199 op_sel:[0,0,1]
	v_cvt_pk_fp8_f32 v211, v202, v203 op_sel:[0,0,1]
	s_nop 0
	global_store_dwordx4 v11, v[208:211], s[14:15]
	ds_read_b32 v170, v8
	ds_read_b32 v171, v8 offset:512
	ds_read_b32 v172, v8 offset:1024
	ds_read_b32 v173, v8 offset:1536
	ds_read_b32 v174, v8 offset:2048
	ds_read_b32 v175, v8 offset:2560
	ds_read_b32 v176, v8 offset:3072
	ds_read_b32 v177, v8 offset:3584
	ds_read_b32 v196, v8 offset:4096
	ds_read_b32 v197, v8 offset:4608
	ds_read_b32 v198, v8 offset:5120
	ds_read_b32 v199, v8 offset:5632
	ds_read_b32 v200, v8 offset:6144
	ds_read_b32 v201, v8 offset:6656
	ds_read_b32 v202, v8 offset:7168
	ds_read_b32 v203, v8 offset:7680
	s_waitcnt lgkmcnt(0)
	v_max_f32_e32 v170, v170, v170
	v_max_f32_e32 v171, v171, v171
	v_max_f32_e32 v172, v172, v172
	v_max_f32_e32 v173, v173, v173
	v_max_f32_e32 v174, v174, v174
	v_max_f32_e32 v175, v175, v175
	v_max_f32_e32 v176, v176, v176
	v_max_f32_e32 v177, v177, v177
	v_max_f32_e32 v196, v196, v196
	v_max_f32_e32 v197, v197, v197
	v_max_f32_e32 v198, v198, v198
	v_max_f32_e32 v199, v199, v199
	v_max_f32_e32 v200, v200, v200
	v_max_f32_e32 v201, v201, v201
	v_max_f32_e32 v202, v202, v202
	v_max_f32_e32 v203, v203, v203
	v_med3_f32 v170, v170, s20, v13
	v_med3_f32 v171, v171, s20, v13
	v_med3_f32 v172, v172, s20, v13
	v_med3_f32 v173, v173, s20, v13
	v_med3_f32 v174, v174, s20, v13
	v_med3_f32 v175, v175, s20, v13
	v_med3_f32 v176, v176, s20, v13
	v_med3_f32 v177, v177, s20, v13
	v_med3_f32 v196, v196, s20, v13
	v_med3_f32 v197, v197, s20, v13
	v_med3_f32 v198, v198, s20, v13
	v_med3_f32 v199, v199, s20, v13
	v_med3_f32 v200, v200, s20, v13
	v_med3_f32 v201, v201, s20, v13
	v_med3_f32 v202, v202, s20, v13
	v_med3_f32 v203, v203, s20, v13
	v_mov_b32_e32 v208, 0
	v_mov_b32_e32 v209, 0
	v_mov_b32_e32 v210, 0
	v_mov_b32_e32 v211, 0
	v_cvt_pk_fp8_f32 v208, v170, v171
	v_cvt_pk_fp8_f32 v209, v174, v175
	v_cvt_pk_fp8_f32 v210, v196, v197
	v_cvt_pk_fp8_f32 v211, v200, v201
	v_cvt_pk_fp8_f32 v208, v172, v173 op_sel:[0,0,1]
	v_cvt_pk_fp8_f32 v209, v176, v177 op_sel:[0,0,1]
	v_cvt_pk_fp8_f32 v210, v198, v199 op_sel:[0,0,1]
	v_cvt_pk_fp8_f32 v211, v202, v203 op_sel:[0,0,1]
	s_nop 0
	global_store_dwordx4 v12, v[208:211], s[14:15]
	s_waitcnt vmcnt(32)
	v_mul_f32_e32 v68, 0x43000000, v68
	v_mul_f32_e32 v69, 0x43000000, v69
	v_mul_f32_e32 v70, 0x43000000, v70
	v_mul_f32_e32 v71, 0x43000000, v71
	ds_write_b128 v5, v[68:71]
	v_mul_f32_e32 v72, 0x43000000, v72
	v_mul_f32_e32 v73, 0x43000000, v73
	v_mul_f32_e32 v74, 0x43000000, v74
	v_mul_f32_e32 v75, 0x43000000, v75
	ds_write_b128 v5, v[72:75] offset:1024
	v_mul_f32_e32 v76, 0x43000000, v76
	v_mul_f32_e32 v77, 0x43000000, v77
	v_mul_f32_e32 v78, 0x43000000, v78
	v_mul_f32_e32 v79, 0x43000000, v79
	ds_write_b128 v5, v[76:79] offset:2048
	v_mul_f32_e32 v80, 0x43000000, v80
	v_mul_f32_e32 v81, 0x43000000, v81
	v_mul_f32_e32 v82, 0x43000000, v82
	v_mul_f32_e32 v83, 0x43000000, v83
	ds_write_b128 v5, v[80:83] offset:3072
	v_mul_f32_e32 v84, 0x43000000, v84
	v_mul_f32_e32 v85, 0x43000000, v85
	v_mul_f32_e32 v86, 0x43000000, v86
	v_mul_f32_e32 v87, 0x43000000, v87
	ds_write_b128 v5, v[84:87] offset:4096
	v_mul_f32_e32 v88, 0x43000000, v88
	v_mul_f32_e32 v89, 0x43000000, v89
	v_mul_f32_e32 v90, 0x43000000, v90
	v_mul_f32_e32 v91, 0x43000000, v91
	ds_write_b128 v5, v[88:91] offset:5120
	v_mul_f32_e32 v92, 0x43000000, v92
	v_mul_f32_e32 v93, 0x43000000, v93
	v_mul_f32_e32 v94, 0x43000000, v94
	v_mul_f32_e32 v95, 0x43000000, v95
	ds_write_b128 v5, v[92:95] offset:6144
	v_mul_f32_e32 v96, 0x43000000, v96
	v_mul_f32_e32 v97, 0x43000000, v97
	v_mul_f32_e32 v98, 0x43000000, v98
	v_mul_f32_e32 v99, 0x43000000, v99
	ds_write_b128 v5, v[96:99] offset:7168
	s_waitcnt lgkmcnt(0)
	s_barrier
; #define GAS __attribute__((address_space(1)))
; #define LAS __attribute__((address_space(3)))
; #define LDS_WAIT() asm volatile("s_waitcnt lgkmcnt(0)" ::: "memory")
; __device__ __forceinline__ unsigned pk4_fp8(float a, float b, float c, float d) {
;     a = fminf(fmaxf(a, -448.f), 448.f); b = fminf(fmaxf(b, -448.f), 448.f); c = fminf(fmaxf(c, -448.f), 448.f); d = fminf(fmaxf(d, -448.f), 448.f);
;     int w = __builtin_amdgcn_cvt_pk_fp8_f32(a, b, 0, false); w = __builtin_amdgcn_cvt_pk_fp8_f32(c, d, w, true); return (unsigned)w; }
;     const int pr = item >> 1, kb = 2 * (pr / nblk) + (item & 1), nb = pr % nblk, k0 = 64 * kb, n0 = 32 * nb;
;     const int nr = n0 + (lane & 31); const int sc = MAP == 1 ? src_col_in(nr) : nr;
;     float v[32];
; #pragma unroll
;     for (int i = 0; i < 32; ++i) v[i] = sc >= 0 ? W[(size_t)(k0 + 2 * i + (lane >> 5)) * Nsrc + sc] : 0.f;
; #pragma unroll
;     for (int i = 0; i < 32; ++i) { const int k = k0 + 2 * i + (lane >> 5); float x = v[i] * wscale; if (KS) x *= (k < ksplit ? ksA[k] : ksB[k - ksplit]); scr[(2 * i + (lane >> 5)) * 33 + (lane & 31)] = x; }
;     LDS_WAIT(); asm volatile("" ::: "memory");
;     const int c = lane & 7;
; #pragma unroll
;     for (int j = 0; j < 4; ++j) { const int n = (lane >> 3) + 8 * j; const LAS float* s = scr + (8 * c) * 33 + n;
;         const unsigned long long o = (unsigned long long)pg8::pk4_fp8(s[0 * 33], s[1 * 33], s[2 * 33], s[3 * 33]) | ((unsigned long long)pg8::pk4_fp8(s[4 * 33], s[5 * 33], s[6 * 33], s[7 * 33]) << 32);
;         *(GAS unsigned long long*)(WT + (size_t)(n0 + n) * K + k0 + 8 * c) = o; }
;     LDS_WAIT(); asm volatile("" ::: "memory");
; }
	s_add_i32 s17, s16, 1632
	s_min_u32 s17, s17, 0xfff
	s_lshr_b32 s18, s17, 5
	s_add_i32 s18, s18, 0
	s_and_b32 s19, s17, 31
	s_lshl_b32 s18, s18, 21
	s_lshl_b32 s19, s19, 9
	s_add_u32 s18, s18, s19
	s_add_u32 s12, s2, s18
	s_addc_u32 s13, s3, 0
	global_load_dwordx4 v[68:71], v10, s[12:13]
	s_add_u32 s12, s12, 0x8000
	s_addc_u32 s13, s13, 0
	global_load_dwordx4 v[72:75], v10, s[12:13]
	s_add_u32 s12, s12, 0x8000
	s_addc_u32 s13, s13, 0
	global_load_dwordx4 v[76:79], v10, s[12:13]
	s_add_u32 s12, s12, 0x8000
	s_addc_u32 s13, s13, 0
	global_load_dwordx4 v[80:83], v10, s[12:13]
	s_add_u32 s12, s12, 0x8000
	s_addc_u32 s13, s13, 0
	global_load_dwordx4 v[84:87], v10, s[12:13]
	s_add_u32 s12, s12, 0x8000
	s_addc_u32 s13, s13, 0
	global_load_dwordx4 v[88:91], v10, s[12:13]
	s_add_u32 s12, s12, 0x8000
	s_addc_u32 s13, s13, 0
	global_load_dwordx4 v[92:95], v10, s[12:13]
	s_add_u32 s12, s12, 0x8000
	s_addc_u32 s13, s13, 0
	global_load_dwordx4 v[96:99], v10, s[12:13]
	s_add_i32 s17, s16, 1248
	s_min_u32 s17, s17, 0xfff
	s_lshr_b32 s18, s17, 5
	s_add_i32 s18, s18, 0
	s_and_b32 s19, s17, 31
	s_lshl_b32 s19, s19, 21
	s_lshl_b32 s18, s18, 7
	s_add_u32 s18, s18, s19
	s_add_u32 s14, s4, s18
	s_addc_u32 s15, s5, 0
	ds_read_b32 v170, v7
	ds_read_b32 v171, v7 offset:512
	ds_read_b32 v172, v7 offset:1024
	ds_read_b32 v173, v7 offset:1536
	ds_read_b32 v174, v7 offset:2048
	ds_read_b32 v175, v7 offset:2560
	ds_read_b32 v176, v7 offset:3072
	ds_read_b32 v177, v7 offset:3584
	ds_read_b32 v196, v7 offset:4096
	ds_read_b32 v197, v7 offset:4608
	ds_read_b32 v198, v7 offset:5120
	ds_read_b32 v199, v7 offset:5632
	ds_read_b32 v200, v7 offset:6144
	ds_read_b32 v201, v7 offset:6656
	ds_read_b32 v202, v7 offset:7168
	ds_read_b32 v203, v7 offset:7680
	s_waitcnt lgkmcnt(0)
	v_max_f32_e32 v170, v170, v170
	v_max_f32_e32 v171, v171, v171
	v_max_f32_e32 v172, v172, v172
	v_max_f32_e32 v173, v173, v173
	v_max_f32_e32 v174, v174, v174
	v_max_f32_e32 v175, v175, v175
	v_max_f32_e32 v176, v176, v176
	v_max_f32_e32 v177, v177, v177
	v_max_f32_e32 v196, v196, v196
	v_max_f32_e32 v197, v197, v197
	v_max_f32_e32 v198, v198, v198
	v_max_f32_e32 v199, v199, v199
	v_max_f32_e32 v200, v200, v200
	v_max_f32_e32 v201, v201, v201
	v_max_f32_e32 v202, v202, v202
	v_max_f32_e32 v203, v203, v203
	v_med3_f32 v170, v170, s20, v13
	v_med3_f32 v171, v171, s20, v13
	v_med3_f32 v172, v172, s20, v13
	v_med3_f32 v173, v173, s20, v13
	v_med3_f32 v174, v174, s20, v13
	v_med3_f32 v175, v175, s20, v13
	v_med3_f32 v176, v176, s20, v13
	v_med3_f32 v177, v177, s20, v13
	v_med3_f32 v196, v196, s20, v13
	v_med3_f32 v197, v197, s20, v13
	v_med3_f32 v198, v198, s20, v13
	v_med3_f32 v199, v199, s20, v13
	v_med3_f32 v200, v200, s20, v13
	v_med3_f32 v201, v201, s20, v13
	v_med3_f32 v202, v202, s20, v13
	v_med3_f32 v203, v203, s20, v13
	v_mov_b32_e32 v208, 0
	v_mov_b32_e32 v209, 0
	v_mov_b32_e32 v210, 0
	v_mov_b32_e32 v211, 0
	v_cvt_pk_fp8_f32 v208, v170, v171
	v_cvt_pk_fp8_f32 v209, v174, v175
	v_cvt_pk_fp8_f32 v210, v196, v197
	v_cvt_pk_fp8_f32 v211, v200, v201
	v_cvt_pk_fp8_f32 v208, v172, v173 op_sel:[0,0,1]
	v_cvt_pk_fp8_f32 v209, v176, v177 op_sel:[0,0,1]
	v_cvt_pk_fp8_f32 v210, v198, v199 op_sel:[0,0,1]
	v_cvt_pk_fp8_f32 v211, v202, v203 op_sel:[0,0,1]
	s_nop 0
	global_store_dwordx4 v11, v[208:211], s[14:15]
	ds_read_b32 v170, v9
	ds_read_b32 v171, v9 offset:512
	ds_read_b32 v172, v9 offset:1024
	ds_read_b32 v173, v9 offset:1536
	ds_read_b32 v174, v9 offset:2048
	ds_read_b32 v175, v9 offset:2560
	ds_read_b32 v176, v9 offset:3072
	ds_read_b32 v177, v9 offset:3584
	ds_read_b32 v196, v9 offset:4096
	ds_read_b32 v197, v9 offset:4608
	ds_read_b32 v198, v9 offset:5120
	ds_read_b32 v199, v9 offset:5632
	ds_read_b32 v200, v9 offset:6144
	ds_read_b32 v201, v9 offset:6656
	ds_read_b32 v202, v9 offset:7168
	ds_read_b32 v203, v9 offset:7680
	s_waitcnt lgkmcnt(0)
	v_max_f32_e32 v170, v170, v170
	v_max_f32_e32 v171, v171, v171
	v_max_f32_e32 v172, v172, v172
	v_max_f32_e32 v173, v173, v173
	v_max_f32_e32 v174, v174, v174
	v_max_f32_e32 v175, v175, v175
	v_max_f32_e32 v176, v176, v176
	v_max_f32_e32 v177, v177, v177
	v_max_f32_e32 v196, v196, v196
	v_max_f32_e32 v197, v197, v197
	v_max_f32_e32 v198, v198, v198
	v_max_f32_e32 v199, v199, v199
	v_max_f32_e32 v200, v200, v200
	v_max_f32_e32 v201, v201, v201
	v_max_f32_e32 v202, v202, v202
	v_max_f32_e32 v203, v203, v203
	v_med3_f32 v170, v170, s20, v13
	v_med3_f32 v171, v171, s20, v13
	v_med3_f32 v172, v172, s20, v13
	v_med3_f32 v173, v173, s20, v13
	v_med3_f32 v174, v174, s20, v13
	v_med3_f32 v175, v175, s20, v13
	v_med3_f32 v176, v176, s20, v13
	v_med3_f32 v177, v177, s20, v13
	v_med3_f32 v196, v196, s20, v13
	v_med3_f32 v197, v197, s20, v13
	v_med3_f32 v198, v198, s20, v13
	v_med3_f32 v199, v199, s20, v13
	v_med3_f32 v200, v200, s20, v13
	v_med3_f32 v201, v201, s20, v13
	v_med3_f32 v202, v202, s20, v13
	v_med3_f32 v203, v203, s20, v13
	v_mov_b32_e32 v208, 0
	v_mov_b32_e32 v209, 0
	v_mov_b32_e32 v210, 0
	v_mov_b32_e32 v211, 0
	v_cvt_pk_fp8_f32 v208, v170, v171
	v_cvt_pk_fp8_f32 v209, v174, v175
	v_cvt_pk_fp8_f32 v210, v196, v197
	v_cvt_pk_fp8_f32 v211, v200, v201
	v_cvt_pk_fp8_f32 v208, v172, v173 op_sel:[0,0,1]
	v_cvt_pk_fp8_f32 v209, v176, v177 op_sel:[0,0,1]
	v_cvt_pk_fp8_f32 v210, v198, v199 op_sel:[0,0,1]
	v_cvt_pk_fp8_f32 v211, v202, v203 op_sel:[0,0,1]
	s_nop 0
	global_store_dwordx4 v12, v[208:211], s[14:15]
	s_waitcnt vmcnt(32)
	v_mul_f32_e32 v100, 0x43000000, v100
	v_mul_f32_e32 v101, 0x43000000, v101
	v_mul_f32_e32 v102, 0x43000000, v102
	v_mul_f32_e32 v103, 0x43000000, v103
	ds_write_b128 v4, v[100:103]
	v_mul_f32_e32 v104, 0x43000000, v104
	v_mul_f32_e32 v105, 0x43000000, v105
	v_mul_f32_e32 v106, 0x43000000, v106
	v_mul_f32_e32 v107, 0x43000000, v107
	ds_write_b128 v4, v[104:107] offset:1024
	v_mul_f32_e32 v108, 0x43000000, v108
	v_mul_f32_e32 v109, 0x43000000, v109
	v_mul_f32_e32 v110, 0x43000000, v110
	v_mul_f32_e32 v111, 0x43000000, v111
	ds_write_b128 v4, v[108:111] offset:2048
	v_mul_f32_e32 v112, 0x43000000, v112
	v_mul_f32_e32 v113, 0x43000000, v113
	v_mul_f32_e32 v114, 0x43000000, v114
	v_mul_f32_e32 v115, 0x43000000, v115
	ds_write_b128 v4, v[112:115] offset:3072
	v_mul_f32_e32 v116, 0x43000000, v116
	v_mul_f32_e32 v117, 0x43000000, v117
	v_mul_f32_e32 v118, 0x43000000, v118
	v_mul_f32_e32 v119, 0x43000000, v119
	ds_write_b128 v4, v[116:119] offset:4096
	v_mul_f32_e32 v120, 0x43000000, v120
	v_mul_f32_e32 v121, 0x43000000, v121
	v_mul_f32_e32 v122, 0x43000000, v122
	v_mul_f32_e32 v123, 0x43000000, v123
	ds_write_b128 v4, v[120:123] offset:5120
	v_mul_f32_e32 v124, 0x43000000, v124
	v_mul_f32_e32 v125, 0x43000000, v125
	v_mul_f32_e32 v126, 0x43000000, v126
	v_mul_f32_e32 v127, 0x43000000, v127
	ds_write_b128 v4, v[124:127] offset:6144
	v_mul_f32_e32 v128, 0x43000000, v128
	v_mul_f32_e32 v129, 0x43000000, v129
	v_mul_f32_e32 v130, 0x43000000, v130
	v_mul_f32_e32 v131, 0x43000000, v131
	ds_write_b128 v4, v[128:131] offset:7168
	s_waitcnt lgkmcnt(0)
	s_barrier
; #define GAS __attribute__((address_space(1)))
; #define LAS __attribute__((address_space(3)))
; #define LDS_WAIT() asm volatile("s_waitcnt lgkmcnt(0)" ::: "memory")
; __device__ __forceinline__ unsigned pk4_fp8(float a, float b, float c, float d) {
;     a = fminf(fmaxf(a, -448.f), 448.f); b = fminf(fmaxf(b, -448.f), 448.f); c = fminf(fmaxf(c, -448.f), 448.f); d = fminf(fmaxf(d, -448.f), 448.f);
;     int w = __builtin_amdgcn_cvt_pk_fp8_f32(a, b, 0, false); w = __builtin_amdgcn_cvt_pk_fp8_f32(c, d, w, true); return (unsigned)w; }
;     const int pr = item >> 1, kb = 2 * (pr / nblk) + (item & 1), nb = pr % nblk, k0 = 64 * kb, n0 = 32 * nb;
;     const int nr = n0 + (lane & 31); const int sc = MAP == 1 ? src_col_in(nr) : nr;
;     float v[32];
; #pragma unroll
;     for (int i = 0; i < 32; ++i) v[i] = sc >= 0 ? W[(size_t)(k0 + 2 * i + (lane >> 5)) * Nsrc + sc] : 0.f;
; #pragma unroll
;     for (int i = 0; i < 32; ++i) { const int k = k0 + 2 * i + (lane >> 5); float x = v[i] * wscale; if (KS) x *= (k < ksplit ? ksA[k] : ksB[k - ksplit]); scr[(2 * i + (lane >> 5)) * 33 + (lane & 31)] = x; }
;     LDS_WAIT(); asm volatile("" ::: "memory");
;     const int c = lane & 7;
; #pragma unroll
;     for (int j = 0; j < 4; ++j) { const int n = (lane >> 3) + 8 * j; const LAS float* s = scr + (8 * c) * 33 + n;
;         const unsigned long long o = (unsigned long long)pg8::pk4_fp8(s[0 * 33], s[1 * 33], s[2 * 33], s[3 * 33]) | ((unsigned long long)pg8::pk4_fp8(s[4 * 33], s[5 * 33], s[6 * 33], s[7 * 33]) << 32);
;         *(GAS unsigned long long*)(WT + (size_t)(n0 + n) * K + k0 + 8 * c) = o; }
;     LDS_WAIT(); asm volatile("" ::: "memory");
; }
	s_add_i32 s17, s16, 1728
	s_min_u32 s17, s17, 0xfff
	s_lshr_b32 s18, s17, 5
	s_add_i32 s18, s18, 0
	s_and_b32 s19, s17, 31
	s_lshl_b32 s18, s18, 21
	s_lshl_b32 s19, s19, 9
	s_add_u32 s18, s18, s19
	s_add_u32 s12, s2, s18
	s_addc_u32 s13, s3, 0
	global_load_dwordx4 v[100:103], v10, s[12:13]
	s_add_u32 s12, s12, 0x8000
	s_addc_u32 s13, s13, 0
	global_load_dwordx4 v[104:107], v10, s[12:13]
	s_add_u32 s12, s12, 0x8000
	s_addc_u32 s13, s13, 0
	global_load_dwordx4 v[108:111], v10, s[12:13]
	s_add_u32 s12, s12, 0x8000
	s_addc_u32 s13, s13, 0
	global_load_dwordx4 v[112:115], v10, s[12:13]
	s_add_u32 s12, s12, 0x8000
	s_addc_u32 s13, s13, 0
	global_load_dwordx4 v[116:119], v10, s[12:13]
	s_add_u32 s12, s12, 0x8000
	s_addc_u32 s13, s13, 0
	global_load_dwordx4 v[120:123], v10, s[12:13]
	s_add_u32 s12, s12, 0x8000
	s_addc_u32 s13, s13, 0
	global_load_dwordx4 v[124:127], v10, s[12:13]
	s_add_u32 s12, s12, 0x8000
	s_addc_u32 s13, s13, 0
	global_load_dwordx4 v[128:131], v10, s[12:13]
	s_add_i32 s17, s16, 1344
	s_min_u32 s17, s17, 0xfff
	s_lshr_b32 s18, s17, 5
	s_add_i32 s18, s18, 0
	s_and_b32 s19, s17, 31
	s_lshl_b32 s19, s19, 21
	s_lshl_b32 s18, s18, 7
	s_add_u32 s18, s18, s19
	s_add_u32 s14, s4, s18
	s_addc_u32 s15, s5, 0
	ds_read_b32 v170, v6
	ds_read_b32 v171, v6 offset:512
	ds_read_b32 v172, v6 offset:1024
	ds_read_b32 v173, v6 offset:1536
	ds_read_b32 v174, v6 offset:2048
	ds_read_b32 v175, v6 offset:2560
	ds_read_b32 v176, v6 offset:3072
	ds_read_b32 v177, v6 offset:3584
	ds_read_b32 v196, v6 offset:4096
	ds_read_b32 v197, v6 offset:4608
	ds_read_b32 v198, v6 offset:5120
	ds_read_b32 v199, v6 offset:5632
	ds_read_b32 v200, v6 offset:6144
	ds_read_b32 v201, v6 offset:6656
	ds_read_b32 v202, v6 offset:7168
	ds_read_b32 v203, v6 offset:7680
	s_waitcnt lgkmcnt(0)
	v_max_f32_e32 v170, v170, v170
	v_max_f32_e32 v171, v171, v171
	v_max_f32_e32 v172, v172, v172
	v_max_f32_e32 v173, v173, v173
	v_max_f32_e32 v174, v174, v174
	v_max_f32_e32 v175, v175, v175
	v_max_f32_e32 v176, v176, v176
	v_max_f32_e32 v177, v177, v177
	v_max_f32_e32 v196, v196, v196
	v_max_f32_e32 v197, v197, v197
	v_max_f32_e32 v198, v198, v198
	v_max_f32_e32 v199, v199, v199
	v_max_f32_e32 v200, v200, v200
	v_max_f32_e32 v201, v201, v201
	v_max_f32_e32 v202, v202, v202
	v_max_f32_e32 v203, v203, v203
	v_med3_f32 v170, v170, s20, v13
	v_med3_f32 v171, v171, s20, v13
	v_med3_f32 v172, v172, s20, v13
	v_med3_f32 v173, v173, s20, v13
	v_med3_f32 v174, v174, s20, v13
	v_med3_f32 v175, v175, s20, v13
	v_med3_f32 v176, v176, s20, v13
	v_med3_f32 v177, v177, s20, v13
	v_med3_f32 v196, v196, s20, v13
	v_med3_f32 v197, v197, s20, v13
	v_med3_f32 v198, v198, s20, v13
	v_med3_f32 v199, v199, s20, v13
	v_med3_f32 v200, v200, s20, v13
	v_med3_f32 v201, v201, s20, v13
	v_med3_f32 v202, v202, s20, v13
	v_med3_f32 v203, v203, s20, v13
	v_mov_b32_e32 v208, 0
	v_mov_b32_e32 v209, 0
	v_mov_b32_e32 v210, 0
	v_mov_b32_e32 v211, 0
	v_cvt_pk_fp8_f32 v208, v170, v171
	v_cvt_pk_fp8_f32 v209, v174, v175
	v_cvt_pk_fp8_f32 v210, v196, v197
	v_cvt_pk_fp8_f32 v211, v200, v201
	v_cvt_pk_fp8_f32 v208, v172, v173 op_sel:[0,0,1]
	v_cvt_pk_fp8_f32 v209, v176, v177 op_sel:[0,0,1]
	v_cvt_pk_fp8_f32 v210, v198, v199 op_sel:[0,0,1]
	v_cvt_pk_fp8_f32 v211, v202, v203 op_sel:[0,0,1]
	s_nop 0
	global_store_dwordx4 v11, v[208:211], s[14:15]
	ds_read_b32 v170, v8
	ds_read_b32 v171, v8 offset:512
	ds_read_b32 v172, v8 offset:1024
	ds_read_b32 v173, v8 offset:1536
	ds_read_b32 v174, v8 offset:2048
	ds_read_b32 v175, v8 offset:2560
	ds_read_b32 v176, v8 offset:3072
	ds_read_b32 v177, v8 offset:3584
	ds_read_b32 v196, v8 offset:4096
	ds_read_b32 v197, v8 offset:4608
	ds_read_b32 v198, v8 offset:5120
	ds_read_b32 v199, v8 offset:5632
	ds_read_b32 v200, v8 offset:6144
	ds_read_b32 v201, v8 offset:6656
	ds_read_b32 v202, v8 offset:7168
	ds_read_b32 v203, v8 offset:7680
	s_waitcnt lgkmcnt(0)
	v_max_f32_e32 v170, v170, v170
	v_max_f32_e32 v171, v171, v171
	v_max_f32_e32 v172, v172, v172
	v_max_f32_e32 v173, v173, v173
	v_max_f32_e32 v174, v174, v174
	v_max_f32_e32 v175, v175, v175
	v_max_f32_e32 v176, v176, v176
	v_max_f32_e32 v177, v177, v177
	v_max_f32_e32 v196, v196, v196
	v_max_f32_e32 v197, v197, v197
	v_max_f32_e32 v198, v198, v198
	v_max_f32_e32 v199, v199, v199
	v_max_f32_e32 v200, v200, v200
	v_max_f32_e32 v201, v201, v201
	v_max_f32_e32 v202, v202, v202
	v_max_f32_e32 v203, v203, v203
	v_med3_f32 v170, v170, s20, v13
	v_med3_f32 v171, v171, s20, v13
	v_med3_f32 v172, v172, s20, v13
	v_med3_f32 v173, v173, s20, v13
	v_med3_f32 v174, v174, s20, v13
	v_med3_f32 v175, v175, s20, v13
	v_med3_f32 v176, v176, s20, v13
	v_med3_f32 v177, v177, s20, v13
	v_med3_f32 v196, v196, s20, v13
	v_med3_f32 v197, v197, s20, v13
	v_med3_f32 v198, v198, s20, v13
	v_med3_f32 v199, v199, s20, v13
	v_med3_f32 v200, v200, s20, v13
	v_med3_f32 v201, v201, s20, v13
	v_med3_f32 v202, v202, s20, v13
	v_med3_f32 v203, v203, s20, v13
	v_mov_b32_e32 v208, 0
	v_mov_b32_e32 v209, 0
	v_mov_b32_e32 v210, 0
	v_mov_b32_e32 v211, 0
	v_cvt_pk_fp8_f32 v208, v170, v171
	v_cvt_pk_fp8_f32 v209, v174, v175
	v_cvt_pk_fp8_f32 v210, v196, v197
	v_cvt_pk_fp8_f32 v211, v200, v201
	v_cvt_pk_fp8_f32 v208, v172, v173 op_sel:[0,0,1]
	v_cvt_pk_fp8_f32 v209, v176, v177 op_sel:[0,0,1]
	v_cvt_pk_fp8_f32 v210, v198, v199 op_sel:[0,0,1]
	v_cvt_pk_fp8_f32 v211, v202, v203 op_sel:[0,0,1]
	s_nop 0
	global_store_dwordx4 v12, v[208:211], s[14:15]
	s_waitcnt vmcnt(32)
	v_mul_f32_e32 v132, 0x43000000, v132
	v_mul_f32_e32 v133, 0x43000000, v133
	v_mul_f32_e32 v134, 0x43000000, v134
	v_mul_f32_e32 v135, 0x43000000, v135
	ds_write_b128 v5, v[132:135]
	v_mul_f32_e32 v136, 0x43000000, v136
	v_mul_f32_e32 v137, 0x43000000, v137
	v_mul_f32_e32 v138, 0x43000000, v138
	v_mul_f32_e32 v139, 0x43000000, v139
	ds_write_b128 v5, v[136:139] offset:1024
	v_mul_f32_e32 v140, 0x43000000, v140
	v_mul_f32_e32 v141, 0x43000000, v141
	v_mul_f32_e32 v142, 0x43000000, v142
	v_mul_f32_e32 v143, 0x43000000, v143
	ds_write_b128 v5, v[140:143] offset:2048
	v_mul_f32_e32 v144, 0x43000000, v144
	v_mul_f32_e32 v145, 0x43000000, v145
	v_mul_f32_e32 v146, 0x43000000, v146
	v_mul_f32_e32 v147, 0x43000000, v147
	ds_write_b128 v5, v[144:147] offset:3072
	v_mul_f32_e32 v148, 0x43000000, v148
	v_mul_f32_e32 v149, 0x43000000, v149
	v_mul_f32_e32 v150, 0x43000000, v150
	v_mul_f32_e32 v151, 0x43000000, v151
	ds_write_b128 v5, v[148:151] offset:4096
	v_mul_f32_e32 v152, 0x43000000, v152
	v_mul_f32_e32 v153, 0x43000000, v153
	v_mul_f32_e32 v154, 0x43000000, v154
	v_mul_f32_e32 v155, 0x43000000, v155
	ds_write_b128 v5, v[152:155] offset:5120
	v_mul_f32_e32 v156, 0x43000000, v156
	v_mul_f32_e32 v157, 0x43000000, v157
	v_mul_f32_e32 v158, 0x43000000, v158
	v_mul_f32_e32 v159, 0x43000000, v159
	ds_write_b128 v5, v[156:159] offset:6144
	v_mul_f32_e32 v160, 0x43000000, v160
	v_mul_f32_e32 v161, 0x43000000, v161
	v_mul_f32_e32 v162, 0x43000000, v162
	v_mul_f32_e32 v163, 0x43000000, v163
	ds_write_b128 v5, v[160:163] offset:7168
	s_waitcnt lgkmcnt(0)
	s_barrier
; #define GAS __attribute__((address_space(1)))
; #define LAS __attribute__((address_space(3)))
; #define LDS_WAIT() asm volatile("s_waitcnt lgkmcnt(0)" ::: "memory")
; __device__ __forceinline__ unsigned pk4_fp8(float a, float b, float c, float d) {
;     a = fminf(fmaxf(a, -448.f), 448.f); b = fminf(fmaxf(b, -448.f), 448.f); c = fminf(fmaxf(c, -448.f), 448.f); d = fminf(fmaxf(d, -448.f), 448.f);
;     int w = __builtin_amdgcn_cvt_pk_fp8_f32(a, b, 0, false); w = __builtin_amdgcn_cvt_pk_fp8_f32(c, d, w, true); return (unsigned)w; }
;     const int pr = item >> 1, kb = 2 * (pr / nblk) + (item & 1), nb = pr % nblk, k0 = 64 * kb, n0 = 32 * nb;
;     const int nr = n0 + (lane & 31); const int sc = MAP == 1 ? src_col_in(nr) : nr;
;     float v[32];
; #pragma unroll
;     for (int i = 0; i < 32; ++i) v[i] = sc >= 0 ? W[(size_t)(k0 + 2 * i + (lane >> 5)) * Nsrc + sc] : 0.f;
; #pragma unroll
;     for (int i = 0; i < 32; ++i) { const int k = k0 + 2 * i + (lane >> 5); float x = v[i] * wscale; if (KS) x *= (k < ksplit ? ksA[k] : ksB[k - ksplit]); scr[(2 * i + (lane >> 5)) * 33 + (lane & 31)] = x; }
;     LDS_WAIT(); asm volatile("" ::: "memory");
;     const int c = lane & 7;
; #pragma unroll
;     for (int j = 0; j < 4; ++j) { const int n = (lane >> 3) + 8 * j; const LAS float* s = scr + (8 * c) * 33 + n;
;         const unsigned long long o = (unsigned long long)pg8::pk4_fp8(s[0 * 33], s[1 * 33], s[2 * 33], s[3 * 33]) | ((unsigned long long)pg8::pk4_fp8(s[4 * 33], s[5 * 33], s[6 * 33], s[7 * 33]) << 32);
;         *(GAS unsigned long long*)(WT + (size_t)(n0 + n) * K + k0 + 8 * c) = o; }
;     LDS_WAIT(); asm volatile("" ::: "memory");
; }
	s_add_i32 s17, s16, 1824
	s_min_u32 s17, s17, 0xfff
	s_lshr_b32 s18, s17, 5
	s_add_i32 s18, s18, 0
	s_and_b32 s19, s17, 31
	s_lshl_b32 s18, s18, 21
	s_lshl_b32 s19, s19, 9
	s_add_u32 s18, s18, s19
	s_add_u32 s12, s2, s18
	s_addc_u32 s13, s3, 0
	global_load_dwordx4 v[132:135], v10, s[12:13]
	s_add_u32 s12, s12, 0x8000
	s_addc_u32 s13, s13, 0
	global_load_dwordx4 v[136:139], v10, s[12:13]
	s_add_u32 s12, s12, 0x8000
	s_addc_u32 s13, s13, 0
	global_load_dwordx4 v[140:143], v10, s[12:13]
	s_add_u32 s12, s12, 0x8000
	s_addc_u32 s13, s13, 0
	global_load_dwordx4 v[144:147], v10, s[12:13]
	s_add_u32 s12, s12, 0x8000
	s_addc_u32 s13, s13, 0
	global_load_dwordx4 v[148:151], v10, s[12:13]
	s_add_u32 s12, s12, 0x8000
	s_addc_u32 s13, s13, 0
	global_load_dwordx4 v[152:155], v10, s[12:13]
	s_add_u32 s12, s12, 0x8000
	s_addc_u32 s13, s13, 0
	global_load_dwordx4 v[156:159], v10, s[12:13]
	s_add_u32 s12, s12, 0x8000
	s_addc_u32 s13, s13, 0
	global_load_dwordx4 v[160:163], v10, s[12:13]
	s_add_i32 s17, s16, 1440
	s_min_u32 s17, s17, 0xfff
	s_lshr_b32 s18, s17, 5
	s_add_i32 s18, s18, 0
	s_and_b32 s19, s17, 31
	s_lshl_b32 s19, s19, 21
	s_lshl_b32 s18, s18, 7
	s_add_u32 s18, s18, s19
	s_add_u32 s14, s4, s18
	s_addc_u32 s15, s5, 0
	ds_read_b32 v170, v7
	ds_read_b32 v171, v7 offset:512
	ds_read_b32 v172, v7 offset:1024
	ds_read_b32 v173, v7 offset:1536
	ds_read_b32 v174, v7 offset:2048
	ds_read_b32 v175, v7 offset:2560
	ds_read_b32 v176, v7 offset:3072
	ds_read_b32 v177, v7 offset:3584
	ds_read_b32 v196, v7 offset:4096
	ds_read_b32 v197, v7 offset:4608
	ds_read_b32 v198, v7 offset:5120
	ds_read_b32 v199, v7 offset:5632
	ds_read_b32 v200, v7 offset:6144
	ds_read_b32 v201, v7 offset:6656
	ds_read_b32 v202, v7 offset:7168
	ds_read_b32 v203, v7 offset:7680
	s_waitcnt lgkmcnt(0)
	v_max_f32_e32 v170, v170, v170
	v_max_f32_e32 v171, v171, v171
	v_max_f32_e32 v172, v172, v172
	v_max_f32_e32 v173, v173, v173
	v_max_f32_e32 v174, v174, v174
	v_max_f32_e32 v175, v175, v175
	v_max_f32_e32 v176, v176, v176
	v_max_f32_e32 v177, v177, v177
	v_max_f32_e32 v196, v196, v196
	v_max_f32_e32 v197, v197, v197
	v_max_f32_e32 v198, v198, v198
	v_max_f32_e32 v199, v199, v199
	v_max_f32_e32 v200, v200, v200
	v_max_f32_e32 v201, v201, v201
	v_max_f32_e32 v202, v202, v202
	v_max_f32_e32 v203, v203, v203
	v_med3_f32 v170, v170, s20, v13
	v_med3_f32 v171, v171, s20, v13
	v_med3_f32 v172, v172, s20, v13
	v_med3_f32 v173, v173, s20, v13
	v_med3_f32 v174, v174, s20, v13
	v_med3_f32 v175, v175, s20, v13
	v_med3_f32 v176, v176, s20, v13
	v_med3_f32 v177, v177, s20, v13
	v_med3_f32 v196, v196, s20, v13
	v_med3_f32 v197, v197, s20, v13
	v_med3_f32 v198, v198, s20, v13
	v_med3_f32 v199, v199, s20, v13
	v_med3_f32 v200, v200, s20, v13
	v_med3_f32 v201, v201, s20, v13
	v_med3_f32 v202, v202, s20, v13
	v_med3_f32 v203, v203, s20, v13
	v_mov_b32_e32 v208, 0
	v_mov_b32_e32 v209, 0
	v_mov_b32_e32 v210, 0
	v_mov_b32_e32 v211, 0
	v_cvt_pk_fp8_f32 v208, v170, v171
	v_cvt_pk_fp8_f32 v209, v174, v175
	v_cvt_pk_fp8_f32 v210, v196, v197
	v_cvt_pk_fp8_f32 v211, v200, v201
	v_cvt_pk_fp8_f32 v208, v172, v173 op_sel:[0,0,1]
	v_cvt_pk_fp8_f32 v209, v176, v177 op_sel:[0,0,1]
	v_cvt_pk_fp8_f32 v210, v198, v199 op_sel:[0,0,1]
	v_cvt_pk_fp8_f32 v211, v202, v203 op_sel:[0,0,1]
	s_nop 0
	global_store_dwordx4 v11, v[208:211], s[14:15]
	ds_read_b32 v170, v9
	ds_read_b32 v171, v9 offset:512
	ds_read_b32 v172, v9 offset:1024
	ds_read_b32 v173, v9 offset:1536
	ds_read_b32 v174, v9 offset:2048
	ds_read_b32 v175, v9 offset:2560
	ds_read_b32 v176, v9 offset:3072
	ds_read_b32 v177, v9 offset:3584
	ds_read_b32 v196, v9 offset:4096
	ds_read_b32 v197, v9 offset:4608
	ds_read_b32 v198, v9 offset:5120
	ds_read_b32 v199, v9 offset:5632
	ds_read_b32 v200, v9 offset:6144
	ds_read_b32 v201, v9 offset:6656
	ds_read_b32 v202, v9 offset:7168
	ds_read_b32 v203, v9 offset:7680
	s_waitcnt lgkmcnt(0)
	v_max_f32_e32 v170, v170, v170
	v_max_f32_e32 v171, v171, v171
	v_max_f32_e32 v172, v172, v172
	v_max_f32_e32 v173, v173, v173
	v_max_f32_e32 v174, v174, v174
	v_max_f32_e32 v175, v175, v175
	v_max_f32_e32 v176, v176, v176
	v_max_f32_e32 v177, v177, v177
	v_max_f32_e32 v196, v196, v196
	v_max_f32_e32 v197, v197, v197
	v_max_f32_e32 v198, v198, v198
	v_max_f32_e32 v199, v199, v199
	v_max_f32_e32 v200, v200, v200
	v_max_f32_e32 v201, v201, v201
	v_max_f32_e32 v202, v202, v202
	v_max_f32_e32 v203, v203, v203
	v_med3_f32 v170, v170, s20, v13
	v_med3_f32 v171, v171, s20, v13
	v_med3_f32 v172, v172, s20, v13
	v_med3_f32 v173, v173, s20, v13
	v_med3_f32 v174, v174, s20, v13
	v_med3_f32 v175, v175, s20, v13
	v_med3_f32 v176, v176, s20, v13
	v_med3_f32 v177, v177, s20, v13
	v_med3_f32 v196, v196, s20, v13
	v_med3_f32 v197, v197, s20, v13
	v_med3_f32 v198, v198, s20, v13
	v_med3_f32 v199, v199, s20, v13
	v_med3_f32 v200, v200, s20, v13
	v_med3_f32 v201, v201, s20, v13
	v_med3_f32 v202, v202, s20, v13
	v_med3_f32 v203, v203, s20, v13
	v_mov_b32_e32 v208, 0
	v_mov_b32_e32 v209, 0
	v_mov_b32_e32 v210, 0
	v_mov_b32_e32 v211, 0
	v_cvt_pk_fp8_f32 v208, v170, v171
	v_cvt_pk_fp8_f32 v209, v174, v175
	v_cvt_pk_fp8_f32 v210, v196, v197
	v_cvt_pk_fp8_f32 v211, v200, v201
	v_cvt_pk_fp8_f32 v208, v172, v173 op_sel:[0,0,1]
	v_cvt_pk_fp8_f32 v209, v176, v177 op_sel:[0,0,1]
	v_cvt_pk_fp8_f32 v210, v198, v199 op_sel:[0,0,1]
	v_cvt_pk_fp8_f32 v211, v202, v203 op_sel:[0,0,1]
	s_nop 0
	global_store_dwordx4 v12, v[208:211], s[14:15]
	s_waitcnt vmcnt(32)
	v_mul_f32_e32 v36, 0x43000000, v36
	v_mul_f32_e32 v37, 0x43000000, v37
	v_mul_f32_e32 v38, 0x43000000, v38
	v_mul_f32_e32 v39, 0x43000000, v39
	ds_write_b128 v4, v[36:39]
	v_mul_f32_e32 v40, 0x43000000, v40
	v_mul_f32_e32 v41, 0x43000000, v41
	v_mul_f32_e32 v42, 0x43000000, v42
	v_mul_f32_e32 v43, 0x43000000, v43
	ds_write_b128 v4, v[40:43] offset:1024
	v_mul_f32_e32 v44, 0x43000000, v44
	v_mul_f32_e32 v45, 0x43000000, v45
	v_mul_f32_e32 v46, 0x43000000, v46
	v_mul_f32_e32 v47, 0x43000000, v47
	ds_write_b128 v4, v[44:47] offset:2048
	v_mul_f32_e32 v48, 0x43000000, v48
	v_mul_f32_e32 v49, 0x43000000, v49
	v_mul_f32_e32 v50, 0x43000000, v50
	v_mul_f32_e32 v51, 0x43000000, v51
	ds_write_b128 v4, v[48:51] offset:3072
	v_mul_f32_e32 v52, 0x43000000, v52
	v_mul_f32_e32 v53, 0x43000000, v53
	v_mul_f32_e32 v54, 0x43000000, v54
	v_mul_f32_e32 v55, 0x43000000, v55
	ds_write_b128 v4, v[52:55] offset:4096
	v_mul_f32_e32 v56, 0x43000000, v56
	v_mul_f32_e32 v57, 0x43000000, v57
	v_mul_f32_e32 v58, 0x43000000, v58
	v_mul_f32_e32 v59, 0x43000000, v59
	ds_write_b128 v4, v[56:59] offset:5120
	v_mul_f32_e32 v60, 0x43000000, v60
	v_mul_f32_e32 v61, 0x43000000, v61
	v_mul_f32_e32 v62, 0x43000000, v62
	v_mul_f32_e32 v63, 0x43000000, v63
	ds_write_b128 v4, v[60:63] offset:6144
	v_mul_f32_e32 v64, 0x43000000, v64
	v_mul_f32_e32 v65, 0x43000000, v65
	v_mul_f32_e32 v66, 0x43000000, v66
	v_mul_f32_e32 v67, 0x43000000, v67
	ds_write_b128 v4, v[64:67] offset:7168
	s_waitcnt lgkmcnt(0)
	s_barrier
; #define GAS __attribute__((address_space(1)))
; #define LAS __attribute__((address_space(3)))
; #define LDS_WAIT() asm volatile("s_waitcnt lgkmcnt(0)" ::: "memory")
; __device__ __forceinline__ unsigned pk4_fp8(float a, float b, float c, float d) {
;     a = fminf(fmaxf(a, -448.f), 448.f); b = fminf(fmaxf(b, -448.f), 448.f); c = fminf(fmaxf(c, -448.f), 448.f); d = fminf(fmaxf(d, -448.f), 448.f);
;     int w = __builtin_amdgcn_cvt_pk_fp8_f32(a, b, 0, false); w = __builtin_amdgcn_cvt_pk_fp8_f32(c, d, w, true); return (unsigned)w; }
;     const int pr = item >> 1, kb = 2 * (pr / nblk) + (item & 1), nb = pr % nblk, k0 = 64 * kb, n0 = 32 * nb;
;     const int nr = n0 + (lane & 31); const int sc = MAP == 1 ? src_col_in(nr) : nr;
;     float v[32];
; #pragma unroll
;     for (int i = 0; i < 32; ++i) v[i] = sc >= 0 ? W[(size_t)(k0 + 2 * i + (lane >> 5)) * Nsrc + sc] : 0.f;
; #pragma unroll
;     for (int i = 0; i < 32; ++i) { const int k = k0 + 2 * i + (lane >> 5); float x = v[i] * wscale; if (KS) x *= (k < ksplit ? ksA[k] : ksB[k - ksplit]); scr[(2 * i + (lane >> 5)) * 33 + (lane & 31)] = x; }
;     LDS_WAIT(); asm volatile("" ::: "memory");
;     const int c = lane & 7;
; #pragma unroll
;     for (int j = 0; j < 4; ++j) { const int n = (lane >> 3) + 8 * j; const LAS float* s = scr + (8 * c) * 33 + n;
;         const unsigned long long o = (unsigned long long)pg8::pk4_fp8(s[0 * 33], s[1 * 33], s[2 * 33], s[3 * 33]) | ((unsigned long long)pg8::pk4_fp8(s[4 * 33], s[5 * 33], s[6 * 33], s[7 * 33]) << 32);
;         *(GAS unsigned long long*)(WT + (size_t)(n0 + n) * K + k0 + 8 * c) = o; }
;     LDS_WAIT(); asm volatile("" ::: "memory");
; }
	s_add_i32 s17, s16, 1920
	s_min_u32 s17, s17, 0xfff
	s_lshr_b32 s18, s17, 5
	s_add_i32 s18, s18, 0
	s_and_b32 s19, s17, 31
	s_lshl_b32 s18, s18, 21
	s_lshl_b32 s19, s19, 9
	s_add_u32 s18, s18, s19
	s_add_u32 s12, s2, s18
	s_addc_u32 s13, s3, 0
	global_load_dwordx4 v[36:39], v10, s[12:13]
	s_add_u32 s12, s12, 0x8000
	s_addc_u32 s13, s13, 0
	global_load_dwordx4 v[40:43], v10, s[12:13]
	s_add_u32 s12, s12, 0x8000
	s_addc_u32 s13, s13, 0
	global_load_dwordx4 v[44:47], v10, s[12:13]
	s_add_u32 s12, s12, 0x8000
	s_addc_u32 s13, s13, 0
	global_load_dwordx4 v[48:51], v10, s[12:13]
	s_add_u32 s12, s12, 0x8000
	s_addc_u32 s13, s13, 0
	global_load_dwordx4 v[52:55], v10, s[12:13]
	s_add_u32 s12, s12, 0x8000
	s_addc_u32 s13, s13, 0
	global_load_dwordx4 v[56:59], v10, s[12:13]
	s_add_u32 s12, s12, 0x8000
	s_addc_u32 s13, s13, 0
	global_load_dwordx4 v[60:63], v10, s[12:13]
	s_add_u32 s12, s12, 0x8000
	s_addc_u32 s13, s13, 0
	global_load_dwordx4 v[64:67], v10, s[12:13]
	s_add_i32 s17, s16, 1536
	s_min_u32 s17, s17, 0xfff
	s_lshr_b32 s18, s17, 5
	s_add_i32 s18, s18, 0
	s_and_b32 s19, s17, 31
	s_lshl_b32 s19, s19, 21
	s_lshl_b32 s18, s18, 7
	s_add_u32 s18, s18, s19
	s_add_u32 s14, s4, s18
	s_addc_u32 s15, s5, 0
	ds_read_b32 v170, v6
	ds_read_b32 v171, v6 offset:512
	ds_read_b32 v172, v6 offset:1024
	ds_read_b32 v173, v6 offset:1536
	ds_read_b32 v174, v6 offset:2048
	ds_read_b32 v175, v6 offset:2560
	ds_read_b32 v176, v6 offset:3072
	ds_read_b32 v177, v6 offset:3584
	ds_read_b32 v196, v6 offset:4096
	ds_read_b32 v197, v6 offset:4608
	ds_read_b32 v198, v6 offset:5120
	ds_read_b32 v199, v6 offset:5632
	ds_read_b32 v200, v6 offset:6144
	ds_read_b32 v201, v6 offset:6656
	ds_read_b32 v202, v6 offset:7168
	ds_read_b32 v203, v6 offset:7680
	s_waitcnt lgkmcnt(0)
	v_max_f32_e32 v170, v170, v170
	v_max_f32_e32 v171, v171, v171
	v_max_f32_e32 v172, v172, v172
	v_max_f32_e32 v173, v173, v173
	v_max_f32_e32 v174, v174, v174
	v_max_f32_e32 v175, v175, v175
	v_max_f32_e32 v176, v176, v176
	v_max_f32_e32 v177, v177, v177
	v_max_f32_e32 v196, v196, v196
	v_max_f32_e32 v197, v197, v197
	v_max_f32_e32 v198, v198, v198
	v_max_f32_e32 v199, v199, v199
	v_max_f32_e32 v200, v200, v200
	v_max_f32_e32 v201, v201, v201
	v_max_f32_e32 v202, v202, v202
	v_max_f32_e32 v203, v203, v203
	v_med3_f32 v170, v170, s20, v13
	v_med3_f32 v171, v171, s20, v13
	v_med3_f32 v172, v172, s20, v13
	v_med3_f32 v173, v173, s20, v13
	v_med3_f32 v174, v174, s20, v13
	v_med3_f32 v175, v175, s20, v13
	v_med3_f32 v176, v176, s20, v13
	v_med3_f32 v177, v177, s20, v13
	v_med3_f32 v196, v196, s20, v13
	v_med3_f32 v197, v197, s20, v13
	v_med3_f32 v198, v198, s20, v13
	v_med3_f32 v199, v199, s20, v13
	v_med3_f32 v200, v200, s20, v13
	v_med3_f32 v201, v201, s20, v13
	v_med3_f32 v202, v202, s20, v13
	v_med3_f32 v203, v203, s20, v13
	v_mov_b32_e32 v208, 0
	v_mov_b32_e32 v209, 0
	v_mov_b32_e32 v210, 0
	v_mov_b32_e32 v211, 0
	v_cvt_pk_fp8_f32 v208, v170, v171
	v_cvt_pk_fp8_f32 v209, v174, v175
	v_cvt_pk_fp8_f32 v210, v196, v197
	v_cvt_pk_fp8_f32 v211, v200, v201
	v_cvt_pk_fp8_f32 v208, v172, v173 op_sel:[0,0,1]
	v_cvt_pk_fp8_f32 v209, v176, v177 op_sel:[0,0,1]
	v_cvt_pk_fp8_f32 v210, v198, v199 op_sel:[0,0,1]
	v_cvt_pk_fp8_f32 v211, v202, v203 op_sel:[0,0,1]
	s_nop 0
	global_store_dwordx4 v11, v[208:211], s[14:15]
	ds_read_b32 v170, v8
	ds_read_b32 v171, v8 offset:512
	ds_read_b32 v172, v8 offset:1024
	ds_read_b32 v173, v8 offset:1536
	ds_read_b32 v174, v8 offset:2048
	ds_read_b32 v175, v8 offset:2560
	ds_read_b32 v176, v8 offset:3072
	ds_read_b32 v177, v8 offset:3584
	ds_read_b32 v196, v8 offset:4096
	ds_read_b32 v197, v8 offset:4608
	ds_read_b32 v198, v8 offset:5120
	ds_read_b32 v199, v8 offset:5632
	ds_read_b32 v200, v8 offset:6144
	ds_read_b32 v201, v8 offset:6656
	ds_read_b32 v202, v8 offset:7168
	ds_read_b32 v203, v8 offset:7680
	s_waitcnt lgkmcnt(0)
	v_max_f32_e32 v170, v170, v170
	v_max_f32_e32 v171, v171, v171
	v_max_f32_e32 v172, v172, v172
	v_max_f32_e32 v173, v173, v173
	v_max_f32_e32 v174, v174, v174
	v_max_f32_e32 v175, v175, v175
	v_max_f32_e32 v176, v176, v176
	v_max_f32_e32 v177, v177, v177
	v_max_f32_e32 v196, v196, v196
	v_max_f32_e32 v197, v197, v197
	v_max_f32_e32 v198, v198, v198
	v_max_f32_e32 v199, v199, v199
	v_max_f32_e32 v200, v200, v200
	v_max_f32_e32 v201, v201, v201
	v_max_f32_e32 v202, v202, v202
	v_max_f32_e32 v203, v203, v203
	v_med3_f32 v170, v170, s20, v13
	v_med3_f32 v171, v171, s20, v13
	v_med3_f32 v172, v172, s20, v13
	v_med3_f32 v173, v173, s20, v13
	v_med3_f32 v174, v174, s20, v13
	v_med3_f32 v175, v175, s20, v13
	v_med3_f32 v176, v176, s20, v13
	v_med3_f32 v177, v177, s20, v13
	v_med3_f32 v196, v196, s20, v13
	v_med3_f32 v197, v197, s20, v13
	v_med3_f32 v198, v198, s20, v13
	v_med3_f32 v199, v199, s20, v13
	v_med3_f32 v200, v200, s20, v13
	v_med3_f32 v201, v201, s20, v13
	v_med3_f32 v202, v202, s20, v13
	v_med3_f32 v203, v203, s20, v13
	v_mov_b32_e32 v208, 0
	v_mov_b32_e32 v209, 0
	v_mov_b32_e32 v210, 0
	v_mov_b32_e32 v211, 0
	v_cvt_pk_fp8_f32 v208, v170, v171
	v_cvt_pk_fp8_f32 v209, v174, v175
	v_cvt_pk_fp8_f32 v210, v196, v197
	v_cvt_pk_fp8_f32 v211, v200, v201
	v_cvt_pk_fp8_f32 v208, v172, v173 op_sel:[0,0,1]
	v_cvt_pk_fp8_f32 v209, v176, v177 op_sel:[0,0,1]
	v_cvt_pk_fp8_f32 v210, v198, v199 op_sel:[0,0,1]
	v_cvt_pk_fp8_f32 v211, v202, v203 op_sel:[0,0,1]
	s_nop 0
	global_store_dwordx4 v12, v[208:211], s[14:15]
	s_waitcnt vmcnt(32)
	v_mul_f32_e32 v68, 0x43000000, v68
	v_mul_f32_e32 v69, 0x43000000, v69
	v_mul_f32_e32 v70, 0x43000000, v70
	v_mul_f32_e32 v71, 0x43000000, v71
	ds_write_b128 v5, v[68:71]
	v_mul_f32_e32 v72, 0x43000000, v72
	v_mul_f32_e32 v73, 0x43000000, v73
	v_mul_f32_e32 v74, 0x43000000, v74
	v_mul_f32_e32 v75, 0x43000000, v75
	ds_write_b128 v5, v[72:75] offset:1024
	v_mul_f32_e32 v76, 0x43000000, v76
	v_mul_f32_e32 v77, 0x43000000, v77
	v_mul_f32_e32 v78, 0x43000000, v78
	v_mul_f32_e32 v79, 0x43000000, v79
	ds_write_b128 v5, v[76:79] offset:2048
	v_mul_f32_e32 v80, 0x43000000, v80
	v_mul_f32_e32 v81, 0x43000000, v81
	v_mul_f32_e32 v82, 0x43000000, v82
	v_mul_f32_e32 v83, 0x43000000, v83
	ds_write_b128 v5, v[80:83] offset:3072
	v_mul_f32_e32 v84, 0x43000000, v84
	v_mul_f32_e32 v85, 0x43000000, v85
	v_mul_f32_e32 v86, 0x43000000, v86
	v_mul_f32_e32 v87, 0x43000000, v87
	ds_write_b128 v5, v[84:87] offset:4096
	v_mul_f32_e32 v88, 0x43000000, v88
	v_mul_f32_e32 v89, 0x43000000, v89
	v_mul_f32_e32 v90, 0x43000000, v90
	v_mul_f32_e32 v91, 0x43000000, v91
	ds_write_b128 v5, v[88:91] offset:5120
	v_mul_f32_e32 v92, 0x43000000, v92
	v_mul_f32_e32 v93, 0x43000000, v93
	v_mul_f32_e32 v94, 0x43000000, v94
	v_mul_f32_e32 v95, 0x43000000, v95
	ds_write_b128 v5, v[92:95] offset:6144
	v_mul_f32_e32 v96, 0x43000000, v96
	v_mul_f32_e32 v97, 0x43000000, v97
	v_mul_f32_e32 v98, 0x43000000, v98
	v_mul_f32_e32 v99, 0x43000000, v99
	ds_write_b128 v5, v[96:99] offset:7168
	s_waitcnt lgkmcnt(0)
	s_barrier
; #define GAS __attribute__((address_space(1)))
; #define LAS __attribute__((address_space(3)))
; #define LDS_WAIT() asm volatile("s_waitcnt lgkmcnt(0)" ::: "memory")
; __device__ __forceinline__ unsigned pk4_fp8(float a, float b, float c, float d) {
;     a = fminf(fmaxf(a, -448.f), 448.f); b = fminf(fmaxf(b, -448.f), 448.f); c = fminf(fmaxf(c, -448.f), 448.f); d = fminf(fmaxf(d, -448.f), 448.f);
;     int w = __builtin_amdgcn_cvt_pk_fp8_f32(a, b, 0, false); w = __builtin_amdgcn_cvt_pk_fp8_f32(c, d, w, true); return (unsigned)w; }
;     const int pr = item >> 1, kb = 2 * (pr / nblk) + (item & 1), nb = pr % nblk, k0 = 64 * kb, n0 = 32 * nb;
;     const int nr = n0 + (lane & 31); const int sc = MAP == 1 ? src_col_in(nr) : nr;
;     float v[32];
; #pragma unroll
;     for (int i = 0; i < 32; ++i) v[i] = sc >= 0 ? W[(size_t)(k0 + 2 * i + (lane >> 5)) * Nsrc + sc] : 0.f;
; #pragma unroll
;     for (int i = 0; i < 32; ++i) { const int k = k0 + 2 * i + (lane >> 5); float x = v[i] * wscale; if (KS) x *= (k < ksplit ? ksA[k] : ksB[k - ksplit]); scr[(2 * i + (lane >> 5)) * 33 + (lane & 31)] = x; }
;     LDS_WAIT(); asm volatile("" ::: "memory");
;     const int c = lane & 7;
; #pragma unroll
;     for (int j = 0; j < 4; ++j) { const int n = (lane >> 3) + 8 * j; const LAS float* s = scr + (8 * c) * 33 + n;
;         const unsigned long long o = (unsigned long long)pg8::pk4_fp8(s[0 * 33], s[1 * 33], s[2 * 33], s[3 * 33]) | ((unsigned long long)pg8::pk4_fp8(s[4 * 33], s[5 * 33], s[6 * 33], s[7 * 33]) << 32);
;         *(GAS unsigned long long*)(WT + (size_t)(n0 + n) * K + k0 + 8 * c) = o; }
;     LDS_WAIT(); asm volatile("" ::: "memory");
; }
	s_add_i32 s17, s16, 2016
	s_min_u32 s17, s17, 0xfff
	s_lshr_b32 s18, s17, 5
	s_add_i32 s18, s18, 0
	s_and_b32 s19, s17, 31
	s_lshl_b32 s18, s18, 21
	s_lshl_b32 s19, s19, 9
	s_add_u32 s18, s18, s19
	s_add_u32 s12, s2, s18
	s_addc_u32 s13, s3, 0
	global_load_dwordx4 v[68:71], v10, s[12:13]
	s_add_u32 s12, s12, 0x8000
	s_addc_u32 s13, s13, 0
	global_load_dwordx4 v[72:75], v10, s[12:13]
	s_add_u32 s12, s12, 0x8000
	s_addc_u32 s13, s13, 0
	global_load_dwordx4 v[76:79], v10, s[12:13]
	s_add_u32 s12, s12, 0x8000
	s_addc_u32 s13, s13, 0
	global_load_dwordx4 v[80:83], v10, s[12:13]
	s_add_u32 s12, s12, 0x8000
	s_addc_u32 s13, s13, 0
	global_load_dwordx4 v[84:87], v10, s[12:13]
	s_add_u32 s12, s12, 0x8000
	s_addc_u32 s13, s13, 0
	global_load_dwordx4 v[88:91], v10, s[12:13]
	s_add_u32 s12, s12, 0x8000
	s_addc_u32 s13, s13, 0
	global_load_dwordx4 v[92:95], v10, s[12:13]
	s_add_u32 s12, s12, 0x8000
	s_addc_u32 s13, s13, 0
	global_load_dwordx4 v[96:99], v10, s[12:13]
	s_add_i32 s17, s16, 1632
	s_min_u32 s17, s17, 0xfff
	s_lshr_b32 s18, s17, 5
	s_add_i32 s18, s18, 0
	s_and_b32 s19, s17, 31
	s_lshl_b32 s19, s19, 21
	s_lshl_b32 s18, s18, 7
	s_add_u32 s18, s18, s19
	s_add_u32 s14, s4, s18
	s_addc_u32 s15, s5, 0
	ds_read_b32 v170, v7
	ds_read_b32 v171, v7 offset:512
	ds_read_b32 v172, v7 offset:1024
	ds_read_b32 v173, v7 offset:1536
	ds_read_b32 v174, v7 offset:2048
	ds_read_b32 v175, v7 offset:2560
	ds_read_b32 v176, v7 offset:3072
	ds_read_b32 v177, v7 offset:3584
	ds_read_b32 v196, v7 offset:4096
	ds_read_b32 v197, v7 offset:4608
	ds_read_b32 v198, v7 offset:5120
	ds_read_b32 v199, v7 offset:5632
	ds_read_b32 v200, v7 offset:6144
	ds_read_b32 v201, v7 offset:6656
	ds_read_b32 v202, v7 offset:7168
	ds_read_b32 v203, v7 offset:7680
	s_waitcnt lgkmcnt(0)
	v_max_f32_e32 v170, v170, v170
	v_max_f32_e32 v171, v171, v171
	v_max_f32_e32 v172, v172, v172
	v_max_f32_e32 v173, v173, v173
	v_max_f32_e32 v174, v174, v174
	v_max_f32_e32 v175, v175, v175
	v_max_f32_e32 v176, v176, v176
	v_max_f32_e32 v177, v177, v177
	v_max_f32_e32 v196, v196, v196
	v_max_f32_e32 v197, v197, v197
	v_max_f32_e32 v198, v198, v198
	v_max_f32_e32 v199, v199, v199
	v_max_f32_e32 v200, v200, v200
	v_max_f32_e32 v201, v201, v201
	v_max_f32_e32 v202, v202, v202
	v_max_f32_e32 v203, v203, v203
	v_med3_f32 v170, v170, s20, v13
	v_med3_f32 v171, v171, s20, v13
	v_med3_f32 v172, v172, s20, v13
	v_med3_f32 v173, v173, s20, v13
	v_med3_f32 v174, v174, s20, v13
	v_med3_f32 v175, v175, s20, v13
	v_med3_f32 v176, v176, s20, v13
	v_med3_f32 v177, v177, s20, v13
	v_med3_f32 v196, v196, s20, v13
	v_med3_f32 v197, v197, s20, v13
	v_med3_f32 v198, v198, s20, v13
	v_med3_f32 v199, v199, s20, v13
	v_med3_f32 v200, v200, s20, v13
	v_med3_f32 v201, v201, s20, v13
	v_med3_f32 v202, v202, s20, v13
	v_med3_f32 v203, v203, s20, v13
	v_mov_b32_e32 v208, 0
	v_mov_b32_e32 v209, 0
	v_mov_b32_e32 v210, 0
	v_mov_b32_e32 v211, 0
	v_cvt_pk_fp8_f32 v208, v170, v171
	v_cvt_pk_fp8_f32 v209, v174, v175
	v_cvt_pk_fp8_f32 v210, v196, v197
	v_cvt_pk_fp8_f32 v211, v200, v201
	v_cvt_pk_fp8_f32 v208, v172, v173 op_sel:[0,0,1]
	v_cvt_pk_fp8_f32 v209, v176, v177 op_sel:[0,0,1]
	v_cvt_pk_fp8_f32 v210, v198, v199 op_sel:[0,0,1]
	v_cvt_pk_fp8_f32 v211, v202, v203 op_sel:[0,0,1]
	s_nop 0
	global_store_dwordx4 v11, v[208:211], s[14:15]
	ds_read_b32 v170, v9
	ds_read_b32 v171, v9 offset:512
	ds_read_b32 v172, v9 offset:1024
	ds_read_b32 v173, v9 offset:1536
	ds_read_b32 v174, v9 offset:2048
	ds_read_b32 v175, v9 offset:2560
	ds_read_b32 v176, v9 offset:3072
	ds_read_b32 v177, v9 offset:3584
	ds_read_b32 v196, v9 offset:4096
	ds_read_b32 v197, v9 offset:4608
	ds_read_b32 v198, v9 offset:5120
	ds_read_b32 v199, v9 offset:5632
	ds_read_b32 v200, v9 offset:6144
	ds_read_b32 v201, v9 offset:6656
	ds_read_b32 v202, v9 offset:7168
	ds_read_b32 v203, v9 offset:7680
	s_waitcnt lgkmcnt(0)
	v_max_f32_e32 v170, v170, v170
	v_max_f32_e32 v171, v171, v171
	v_max_f32_e32 v172, v172, v172
	v_max_f32_e32 v173, v173, v173
	v_max_f32_e32 v174, v174, v174
	v_max_f32_e32 v175, v175, v175
	v_max_f32_e32 v176, v176, v176
	v_max_f32_e32 v177, v177, v177
	v_max_f32_e32 v196, v196, v196
	v_max_f32_e32 v197, v197, v197
	v_max_f32_e32 v198, v198, v198
	v_max_f32_e32 v199, v199, v199
	v_max_f32_e32 v200, v200, v200
	v_max_f32_e32 v201, v201, v201
	v_max_f32_e32 v202, v202, v202
	v_max_f32_e32 v203, v203, v203
	v_med3_f32 v170, v170, s20, v13
	v_med3_f32 v171, v171, s20, v13
	v_med3_f32 v172, v172, s20, v13
	v_med3_f32 v173, v173, s20, v13
	v_med3_f32 v174, v174, s20, v13
	v_med3_f32 v175, v175, s20, v13
	v_med3_f32 v176, v176, s20, v13
	v_med3_f32 v177, v177, s20, v13
	v_med3_f32 v196, v196, s20, v13
	v_med3_f32 v197, v197, s20, v13
	v_med3_f32 v198, v198, s20, v13
	v_med3_f32 v199, v199, s20, v13
	v_med3_f32 v200, v200, s20, v13
	v_med3_f32 v201, v201, s20, v13
	v_med3_f32 v202, v202, s20, v13
	v_med3_f32 v203, v203, s20, v13
	v_mov_b32_e32 v208, 0
	v_mov_b32_e32 v209, 0
	v_mov_b32_e32 v210, 0
	v_mov_b32_e32 v211, 0
	v_cvt_pk_fp8_f32 v208, v170, v171
	v_cvt_pk_fp8_f32 v209, v174, v175
	v_cvt_pk_fp8_f32 v210, v196, v197
	v_cvt_pk_fp8_f32 v211, v200, v201
	v_cvt_pk_fp8_f32 v208, v172, v173 op_sel:[0,0,1]
	v_cvt_pk_fp8_f32 v209, v176, v177 op_sel:[0,0,1]
	v_cvt_pk_fp8_f32 v210, v198, v199 op_sel:[0,0,1]
	v_cvt_pk_fp8_f32 v211, v202, v203 op_sel:[0,0,1]
	s_nop 0
	global_store_dwordx4 v12, v[208:211], s[14:15]
	s_waitcnt vmcnt(32)
	v_mul_f32_e32 v100, 0x43000000, v100
	v_mul_f32_e32 v101, 0x43000000, v101
	v_mul_f32_e32 v102, 0x43000000, v102
	v_mul_f32_e32 v103, 0x43000000, v103
	ds_write_b128 v4, v[100:103]
	v_mul_f32_e32 v104, 0x43000000, v104
	v_mul_f32_e32 v105, 0x43000000, v105
	v_mul_f32_e32 v106, 0x43000000, v106
	v_mul_f32_e32 v107, 0x43000000, v107
	ds_write_b128 v4, v[104:107] offset:1024
	v_mul_f32_e32 v108, 0x43000000, v108
	v_mul_f32_e32 v109, 0x43000000, v109
	v_mul_f32_e32 v110, 0x43000000, v110
	v_mul_f32_e32 v111, 0x43000000, v111
	ds_write_b128 v4, v[108:111] offset:2048
	v_mul_f32_e32 v112, 0x43000000, v112
	v_mul_f32_e32 v113, 0x43000000, v113
	v_mul_f32_e32 v114, 0x43000000, v114
	v_mul_f32_e32 v115, 0x43000000, v115
	ds_write_b128 v4, v[112:115] offset:3072
	v_mul_f32_e32 v116, 0x43000000, v116
	v_mul_f32_e32 v117, 0x43000000, v117
	v_mul_f32_e32 v118, 0x43000000, v118
	v_mul_f32_e32 v119, 0x43000000, v119
	ds_write_b128 v4, v[116:119] offset:4096
	v_mul_f32_e32 v120, 0x43000000, v120
	v_mul_f32_e32 v121, 0x43000000, v121
	v_mul_f32_e32 v122, 0x43000000, v122
	v_mul_f32_e32 v123, 0x43000000, v123
	ds_write_b128 v4, v[120:123] offset:5120
	v_mul_f32_e32 v124, 0x43000000, v124
	v_mul_f32_e32 v125, 0x43000000, v125
	v_mul_f32_e32 v126, 0x43000000, v126
	v_mul_f32_e32 v127, 0x43000000, v127
	ds_write_b128 v4, v[124:127] offset:6144
	v_mul_f32_e32 v128, 0x43000000, v128
	v_mul_f32_e32 v129, 0x43000000, v129
	v_mul_f32_e32 v130, 0x43000000, v130
	v_mul_f32_e32 v131, 0x43000000, v131
	ds_write_b128 v4, v[128:131] offset:7168
	s_waitcnt lgkmcnt(0)
	s_barrier
; #define GAS __attribute__((address_space(1)))
; #define LAS __attribute__((address_space(3)))
; #define LDS_WAIT() asm volatile("s_waitcnt lgkmcnt(0)" ::: "memory")
; __device__ __forceinline__ unsigned pk4_fp8(float a, float b, float c, float d) {
;     a = fminf(fmaxf(a, -448.f), 448.f); b = fminf(fmaxf(b, -448.f), 448.f); c = fminf(fmaxf(c, -448.f), 448.f); d = fminf(fmaxf(d, -448.f), 448.f);
;     int w = __builtin_amdgcn_cvt_pk_fp8_f32(a, b, 0, false); w = __builtin_amdgcn_cvt_pk_fp8_f32(c, d, w, true); return (unsigned)w; }
;     const int pr = item >> 1, kb = 2 * (pr / nblk) + (item & 1), nb = pr % nblk, k0 = 64 * kb, n0 = 32 * nb;
;     const int nr = n0 + (lane & 31); const int sc = MAP == 1 ? src_col_in(nr) : nr;
;     float v[32];
; #pragma unroll
;     for (int i = 0; i < 32; ++i) v[i] = sc >= 0 ? W[(size_t)(k0 + 2 * i + (lane >> 5)) * Nsrc + sc] : 0.f;
; #pragma unroll
;     for (int i = 0; i < 32; ++i) { const int k = k0 + 2 * i + (lane >> 5); float x = v[i] * wscale; if (KS) x *= (k < ksplit ? ksA[k] : ksB[k - ksplit]); scr[(2 * i + (lane >> 5)) * 33 + (lane & 31)] = x; }
;     LDS_WAIT(); asm volatile("" ::: "memory");
;     const int c = lane & 7;
; #pragma unroll
;     for (int j = 0; j < 4; ++j) { const int n = (lane >> 3) + 8 * j; const LAS float* s = scr + (8 * c) * 33 + n;
;         const unsigned long long o = (unsigned long long)pg8::pk4_fp8(s[0 * 33], s[1 * 33], s[2 * 33], s[3 * 33]) | ((unsigned long long)pg8::pk4_fp8(s[4 * 33], s[5 * 33], s[6 * 33], s[7 * 33]) << 32);
;         *(GAS unsigned long long*)(WT + (size_t)(n0 + n) * K + k0 + 8 * c) = o; }
;     LDS_WAIT(); asm volatile("" ::: "memory");
; }
	s_add_i32 s17, s16, 2112
	s_min_u32 s17, s17, 0xfff
	s_lshr_b32 s18, s17, 5
	s_add_i32 s18, s18, 0
	s_and_b32 s19, s17, 31
	s_lshl_b32 s18, s18, 21
	s_lshl_b32 s19, s19, 9
	s_add_u32 s18, s18, s19
	s_add_u32 s12, s2, s18
	s_addc_u32 s13, s3, 0
	global_load_dwordx4 v[100:103], v10, s[12:13]
	s_add_u32 s12, s12, 0x8000
	s_addc_u32 s13, s13, 0
	global_load_dwordx4 v[104:107], v10, s[12:13]
	s_add_u32 s12, s12, 0x8000
	s_addc_u32 s13, s13, 0
	global_load_dwordx4 v[108:111], v10, s[12:13]
	s_add_u32 s12, s12, 0x8000
	s_addc_u32 s13, s13, 0
	global_load_dwordx4 v[112:115], v10, s[12:13]
	s_add_u32 s12, s12, 0x8000
	s_addc_u32 s13, s13, 0
	global_load_dwordx4 v[116:119], v10, s[12:13]
	s_add_u32 s12, s12, 0x8000
	s_addc_u32 s13, s13, 0
	global_load_dwordx4 v[120:123], v10, s[12:13]
	s_add_u32 s12, s12, 0x8000
	s_addc_u32 s13, s13, 0
	global_load_dwordx4 v[124:127], v10, s[12:13]
	s_add_u32 s12, s12, 0x8000
	s_addc_u32 s13, s13, 0
	global_load_dwordx4 v[128:131], v10, s[12:13]
	s_add_i32 s17, s16, 1728
	s_min_u32 s17, s17, 0xfff
	s_lshr_b32 s18, s17, 5
	s_add_i32 s18, s18, 0
	s_and_b32 s19, s17, 31
	s_lshl_b32 s19, s19, 21
	s_lshl_b32 s18, s18, 7
	s_add_u32 s18, s18, s19
	s_add_u32 s14, s4, s18
	s_addc_u32 s15, s5, 0
	ds_read_b32 v170, v6
	ds_read_b32 v171, v6 offset:512
	ds_read_b32 v172, v6 offset:1024
	ds_read_b32 v173, v6 offset:1536
	ds_read_b32 v174, v6 offset:2048
	ds_read_b32 v175, v6 offset:2560
	ds_read_b32 v176, v6 offset:3072
	ds_read_b32 v177, v6 offset:3584
	ds_read_b32 v196, v6 offset:4096
	ds_read_b32 v197, v6 offset:4608
	ds_read_b32 v198, v6 offset:5120
	ds_read_b32 v199, v6 offset:5632
	ds_read_b32 v200, v6 offset:6144
	ds_read_b32 v201, v6 offset:6656
	ds_read_b32 v202, v6 offset:7168
	ds_read_b32 v203, v6 offset:7680
	s_waitcnt lgkmcnt(0)
	v_max_f32_e32 v170, v170, v170
	v_max_f32_e32 v171, v171, v171
	v_max_f32_e32 v172, v172, v172
	v_max_f32_e32 v173, v173, v173
	v_max_f32_e32 v174, v174, v174
	v_max_f32_e32 v175, v175, v175
	v_max_f32_e32 v176, v176, v176
	v_max_f32_e32 v177, v177, v177
	v_max_f32_e32 v196, v196, v196
	v_max_f32_e32 v197, v197, v197
	v_max_f32_e32 v198, v198, v198
	v_max_f32_e32 v199, v199, v199
	v_max_f32_e32 v200, v200, v200
	v_max_f32_e32 v201, v201, v201
	v_max_f32_e32 v202, v202, v202
	v_max_f32_e32 v203, v203, v203
	v_med3_f32 v170, v170, s20, v13
	v_med3_f32 v171, v171, s20, v13
	v_med3_f32 v172, v172, s20, v13
	v_med3_f32 v173, v173, s20, v13
	v_med3_f32 v174, v174, s20, v13
	v_med3_f32 v175, v175, s20, v13
	v_med3_f32 v176, v176, s20, v13
	v_med3_f32 v177, v177, s20, v13
	v_med3_f32 v196, v196, s20, v13
	v_med3_f32 v197, v197, s20, v13
	v_med3_f32 v198, v198, s20, v13
	v_med3_f32 v199, v199, s20, v13
	v_med3_f32 v200, v200, s20, v13
	v_med3_f32 v201, v201, s20, v13
	v_med3_f32 v202, v202, s20, v13
	v_med3_f32 v203, v203, s20, v13
	v_mov_b32_e32 v208, 0
	v_mov_b32_e32 v209, 0
	v_mov_b32_e32 v210, 0
	v_mov_b32_e32 v211, 0
	v_cvt_pk_fp8_f32 v208, v170, v171
	v_cvt_pk_fp8_f32 v209, v174, v175
	v_cvt_pk_fp8_f32 v210, v196, v197
	v_cvt_pk_fp8_f32 v211, v200, v201
	v_cvt_pk_fp8_f32 v208, v172, v173 op_sel:[0,0,1]
	v_cvt_pk_fp8_f32 v209, v176, v177 op_sel:[0,0,1]
	v_cvt_pk_fp8_f32 v210, v198, v199 op_sel:[0,0,1]
	v_cvt_pk_fp8_f32 v211, v202, v203 op_sel:[0,0,1]
	s_nop 0
	global_store_dwordx4 v11, v[208:211], s[14:15]
	ds_read_b32 v170, v8
	ds_read_b32 v171, v8 offset:512
	ds_read_b32 v172, v8 offset:1024
	ds_read_b32 v173, v8 offset:1536
	ds_read_b32 v174, v8 offset:2048
	ds_read_b32 v175, v8 offset:2560
	ds_read_b32 v176, v8 offset:3072
	ds_read_b32 v177, v8 offset:3584
	ds_read_b32 v196, v8 offset:4096
	ds_read_b32 v197, v8 offset:4608
	ds_read_b32 v198, v8 offset:5120
	ds_read_b32 v199, v8 offset:5632
	ds_read_b32 v200, v8 offset:6144
	ds_read_b32 v201, v8 offset:6656
	ds_read_b32 v202, v8 offset:7168
	ds_read_b32 v203, v8 offset:7680
	s_waitcnt lgkmcnt(0)
	v_max_f32_e32 v170, v170, v170
	v_max_f32_e32 v171, v171, v171
	v_max_f32_e32 v172, v172, v172
	v_max_f32_e32 v173, v173, v173
	v_max_f32_e32 v174, v174, v174
	v_max_f32_e32 v175, v175, v175
	v_max_f32_e32 v176, v176, v176
	v_max_f32_e32 v177, v177, v177
	v_max_f32_e32 v196, v196, v196
	v_max_f32_e32 v197, v197, v197
	v_max_f32_e32 v198, v198, v198
	v_max_f32_e32 v199, v199, v199
	v_max_f32_e32 v200, v200, v200
	v_max_f32_e32 v201, v201, v201
	v_max_f32_e32 v202, v202, v202
	v_max_f32_e32 v203, v203, v203
	v_med3_f32 v170, v170, s20, v13
	v_med3_f32 v171, v171, s20, v13
	v_med3_f32 v172, v172, s20, v13
	v_med3_f32 v173, v173, s20, v13
	v_med3_f32 v174, v174, s20, v13
	v_med3_f32 v175, v175, s20, v13
	v_med3_f32 v176, v176, s20, v13
	v_med3_f32 v177, v177, s20, v13
	v_med3_f32 v196, v196, s20, v13
	v_med3_f32 v197, v197, s20, v13
	v_med3_f32 v198, v198, s20, v13
	v_med3_f32 v199, v199, s20, v13
	v_med3_f32 v200, v200, s20, v13
	v_med3_f32 v201, v201, s20, v13
	v_med3_f32 v202, v202, s20, v13
	v_med3_f32 v203, v203, s20, v13
	v_mov_b32_e32 v208, 0
	v_mov_b32_e32 v209, 0
	v_mov_b32_e32 v210, 0
	v_mov_b32_e32 v211, 0
	v_cvt_pk_fp8_f32 v208, v170, v171
	v_cvt_pk_fp8_f32 v209, v174, v175
	v_cvt_pk_fp8_f32 v210, v196, v197
	v_cvt_pk_fp8_f32 v211, v200, v201
	v_cvt_pk_fp8_f32 v208, v172, v173 op_sel:[0,0,1]
	v_cvt_pk_fp8_f32 v209, v176, v177 op_sel:[0,0,1]
	v_cvt_pk_fp8_f32 v210, v198, v199 op_sel:[0,0,1]
	v_cvt_pk_fp8_f32 v211, v202, v203 op_sel:[0,0,1]
	s_nop 0
	global_store_dwordx4 v12, v[208:211], s[14:15]
	s_waitcnt vmcnt(32)
	v_mul_f32_e32 v132, 0x43000000, v132
	v_mul_f32_e32 v133, 0x43000000, v133
	v_mul_f32_e32 v134, 0x43000000, v134
	v_mul_f32_e32 v135, 0x43000000, v135
	ds_write_b128 v5, v[132:135]
	v_mul_f32_e32 v136, 0x43000000, v136
	v_mul_f32_e32 v137, 0x43000000, v137
	v_mul_f32_e32 v138, 0x43000000, v138
	v_mul_f32_e32 v139, 0x43000000, v139
	ds_write_b128 v5, v[136:139] offset:1024
	v_mul_f32_e32 v140, 0x43000000, v140
	v_mul_f32_e32 v141, 0x43000000, v141
	v_mul_f32_e32 v142, 0x43000000, v142
	v_mul_f32_e32 v143, 0x43000000, v143
	ds_write_b128 v5, v[140:143] offset:2048
	v_mul_f32_e32 v144, 0x43000000, v144
	v_mul_f32_e32 v145, 0x43000000, v145
	v_mul_f32_e32 v146, 0x43000000, v146
	v_mul_f32_e32 v147, 0x43000000, v147
	ds_write_b128 v5, v[144:147] offset:3072
	v_mul_f32_e32 v148, 0x43000000, v148
	v_mul_f32_e32 v149, 0x43000000, v149
	v_mul_f32_e32 v150, 0x43000000, v150
	v_mul_f32_e32 v151, 0x43000000, v151
	ds_write_b128 v5, v[148:151] offset:4096
	v_mul_f32_e32 v152, 0x43000000, v152
	v_mul_f32_e32 v153, 0x43000000, v153
	v_mul_f32_e32 v154, 0x43000000, v154
	v_mul_f32_e32 v155, 0x43000000, v155
	ds_write_b128 v5, v[152:155] offset:5120
	v_mul_f32_e32 v156, 0x43000000, v156
	v_mul_f32_e32 v157, 0x43000000, v157
	v_mul_f32_e32 v158, 0x43000000, v158
	v_mul_f32_e32 v159, 0x43000000, v159
	ds_write_b128 v5, v[156:159] offset:6144
	v_mul_f32_e32 v160, 0x43000000, v160
	v_mul_f32_e32 v161, 0x43000000, v161
	v_mul_f32_e32 v162, 0x43000000, v162
	v_mul_f32_e32 v163, 0x43000000, v163
	ds_write_b128 v5, v[160:163] offset:7168
	s_waitcnt lgkmcnt(0)
	s_barrier
; #define GAS __attribute__((address_space(1)))
; #define LAS __attribute__((address_space(3)))
; #define LDS_WAIT() asm volatile("s_waitcnt lgkmcnt(0)" ::: "memory")
; __device__ __forceinline__ unsigned pk4_fp8(float a, float b, float c, float d) {
;     a = fminf(fmaxf(a, -448.f), 448.f); b = fminf(fmaxf(b, -448.f), 448.f); c = fminf(fmaxf(c, -448.f), 448.f); d = fminf(fmaxf(d, -448.f), 448.f);
;     int w = __builtin_amdgcn_cvt_pk_fp8_f32(a, b, 0, false); w = __builtin_amdgcn_cvt_pk_fp8_f32(c, d, w, true); return (unsigned)w; }
;     const int pr = item >> 1, kb = 2 * (pr / nblk) + (item & 1), nb = pr % nblk, k0 = 64 * kb, n0 = 32 * nb;
;     const int nr = n0 + (lane & 31); const int sc = MAP == 1 ? src_col_in(nr) : nr;
;     float v[32];
; #pragma unroll
;     for (int i = 0; i < 32; ++i) v[i] = sc >= 0 ? W[(size_t)(k0 + 2 * i + (lane >> 5)) * Nsrc + sc] : 0.f;
; #pragma unroll
;     for (int i = 0; i < 32; ++i) { const int k = k0 + 2 * i + (lane >> 5); float x = v[i] * wscale; if (KS) x *= (k < ksplit ? ksA[k] : ksB[k - ksplit]); scr[(2 * i + (lane >> 5)) * 33 + (lane & 31)] = x; }
;     LDS_WAIT(); asm volatile("" ::: "memory");
;     const int c = lane & 7;
; #pragma unroll
;     for (int j = 0; j < 4; ++j) { const int n = (lane >> 3) + 8 * j; const LAS float* s = scr + (8 * c) * 33 + n;
;         const unsigned long long o = (unsigned long long)pg8::pk4_fp8(s[0 * 33], s[1 * 33], s[2 * 33], s[3 * 33]) | ((unsigned long long)pg8::pk4_fp8(s[4 * 33], s[5 * 33], s[6 * 33], s[7 * 33]) << 32);
;         *(GAS unsigned long long*)(WT + (size_t)(n0 + n) * K + k0 + 8 * c) = o; }
;     LDS_WAIT(); asm volatile("" ::: "memory");
; }
	s_add_i32 s17, s16, 2208
	s_min_u32 s17, s17, 0xfff
	s_lshr_b32 s18, s17, 5
	s_add_i32 s18, s18, 0
	s_and_b32 s19, s17, 31
	s_lshl_b32 s18, s18, 21
	s_lshl_b32 s19, s19, 9
	s_add_u32 s18, s18, s19
	s_add_u32 s12, s2, s18
	s_addc_u32 s13, s3, 0
	global_load_dwordx4 v[132:135], v10, s[12:13]
	s_add_u32 s12, s12, 0x8000
	s_addc_u32 s13, s13, 0
	global_load_dwordx4 v[136:139], v10, s[12:13]
	s_add_u32 s12, s12, 0x8000
	s_addc_u32 s13, s13, 0
	global_load_dwordx4 v[140:143], v10, s[12:13]
	s_add_u32 s12, s12, 0x8000
	s_addc_u32 s13, s13, 0
	global_load_dwordx4 v[144:147], v10, s[12:13]
	s_add_u32 s12, s12, 0x8000
	s_addc_u32 s13, s13, 0
	global_load_dwordx4 v[148:151], v10, s[12:13]
	s_add_u32 s12, s12, 0x8000
	s_addc_u32 s13, s13, 0
	global_load_dwordx4 v[152:155], v10, s[12:13]
	s_add_u32 s12, s12, 0x8000
	s_addc_u32 s13, s13, 0
	global_load_dwordx4 v[156:159], v10, s[12:13]
	s_add_u32 s12, s12, 0x8000
	s_addc_u32 s13, s13, 0
	global_load_dwordx4 v[160:163], v10, s[12:13]
	s_add_i32 s17, s16, 1824
	s_min_u32 s17, s17, 0xfff
	s_lshr_b32 s18, s17, 5
	s_add_i32 s18, s18, 0
	s_and_b32 s19, s17, 31
	s_lshl_b32 s19, s19, 21
	s_lshl_b32 s18, s18, 7
	s_add_u32 s18, s18, s19
	s_add_u32 s14, s4, s18
	s_addc_u32 s15, s5, 0
	ds_read_b32 v170, v7
	ds_read_b32 v171, v7 offset:512
	ds_read_b32 v172, v7 offset:1024
	ds_read_b32 v173, v7 offset:1536
	ds_read_b32 v174, v7 offset:2048
	ds_read_b32 v175, v7 offset:2560
	ds_read_b32 v176, v7 offset:3072
	ds_read_b32 v177, v7 offset:3584
	ds_read_b32 v196, v7 offset:4096
	ds_read_b32 v197, v7 offset:4608
	ds_read_b32 v198, v7 offset:5120
	ds_read_b32 v199, v7 offset:5632
	ds_read_b32 v200, v7 offset:6144
	ds_read_b32 v201, v7 offset:6656
	ds_read_b32 v202, v7 offset:7168
	ds_read_b32 v203, v7 offset:7680
	s_waitcnt lgkmcnt(0)
	v_max_f32_e32 v170, v170, v170
	v_max_f32_e32 v171, v171, v171
	v_max_f32_e32 v172, v172, v172
	v_max_f32_e32 v173, v173, v173
	v_max_f32_e32 v174, v174, v174
	v_max_f32_e32 v175, v175, v175
	v_max_f32_e32 v176, v176, v176
	v_max_f32_e32 v177, v177, v177
	v_max_f32_e32 v196, v196, v196
	v_max_f32_e32 v197, v197, v197
	v_max_f32_e32 v198, v198, v198
	v_max_f32_e32 v199, v199, v199
	v_max_f32_e32 v200, v200, v200
	v_max_f32_e32 v201, v201, v201
	v_max_f32_e32 v202, v202, v202
	v_max_f32_e32 v203, v203, v203
	v_med3_f32 v170, v170, s20, v13
	v_med3_f32 v171, v171, s20, v13
	v_med3_f32 v172, v172, s20, v13
	v_med3_f32 v173, v173, s20, v13
	v_med3_f32 v174, v174, s20, v13
	v_med3_f32 v175, v175, s20, v13
	v_med3_f32 v176, v176, s20, v13
	v_med3_f32 v177, v177, s20, v13
	v_med3_f32 v196, v196, s20, v13
	v_med3_f32 v197, v197, s20, v13
	v_med3_f32 v198, v198, s20, v13
	v_med3_f32 v199, v199, s20, v13
	v_med3_f32 v200, v200, s20, v13
	v_med3_f32 v201, v201, s20, v13
	v_med3_f32 v202, v202, s20, v13
	v_med3_f32 v203, v203, s20, v13
	v_mov_b32_e32 v208, 0
	v_mov_b32_e32 v209, 0
	v_mov_b32_e32 v210, 0
	v_mov_b32_e32 v211, 0
	v_cvt_pk_fp8_f32 v208, v170, v171
	v_cvt_pk_fp8_f32 v209, v174, v175
	v_cvt_pk_fp8_f32 v210, v196, v197
	v_cvt_pk_fp8_f32 v211, v200, v201
	v_cvt_pk_fp8_f32 v208, v172, v173 op_sel:[0,0,1]
	v_cvt_pk_fp8_f32 v209, v176, v177 op_sel:[0,0,1]
	v_cvt_pk_fp8_f32 v210, v198, v199 op_sel:[0,0,1]
	v_cvt_pk_fp8_f32 v211, v202, v203 op_sel:[0,0,1]
	s_nop 0
	global_store_dwordx4 v11, v[208:211], s[14:15]
	ds_read_b32 v170, v9
	ds_read_b32 v171, v9 offset:512
	ds_read_b32 v172, v9 offset:1024
	ds_read_b32 v173, v9 offset:1536
	ds_read_b32 v174, v9 offset:2048
	ds_read_b32 v175, v9 offset:2560
	ds_read_b32 v176, v9 offset:3072
	ds_read_b32 v177, v9 offset:3584
	ds_read_b32 v196, v9 offset:4096
	ds_read_b32 v197, v9 offset:4608
	ds_read_b32 v198, v9 offset:5120
	ds_read_b32 v199, v9 offset:5632
	ds_read_b32 v200, v9 offset:6144
	ds_read_b32 v201, v9 offset:6656
	ds_read_b32 v202, v9 offset:7168
	ds_read_b32 v203, v9 offset:7680
	s_waitcnt lgkmcnt(0)
	v_max_f32_e32 v170, v170, v170
	v_max_f32_e32 v171, v171, v171
	v_max_f32_e32 v172, v172, v172
	v_max_f32_e32 v173, v173, v173
	v_max_f32_e32 v174, v174, v174
	v_max_f32_e32 v175, v175, v175
	v_max_f32_e32 v176, v176, v176
	v_max_f32_e32 v177, v177, v177
	v_max_f32_e32 v196, v196, v196
	v_max_f32_e32 v197, v197, v197
	v_max_f32_e32 v198, v198, v198
	v_max_f32_e32 v199, v199, v199
	v_max_f32_e32 v200, v200, v200
	v_max_f32_e32 v201, v201, v201
	v_max_f32_e32 v202, v202, v202
	v_max_f32_e32 v203, v203, v203
	v_med3_f32 v170, v170, s20, v13
	v_med3_f32 v171, v171, s20, v13
	v_med3_f32 v172, v172, s20, v13
	v_med3_f32 v173, v173, s20, v13
	v_med3_f32 v174, v174, s20, v13
	v_med3_f32 v175, v175, s20, v13
	v_med3_f32 v176, v176, s20, v13
	v_med3_f32 v177, v177, s20, v13
	v_med3_f32 v196, v196, s20, v13
	v_med3_f32 v197, v197, s20, v13
	v_med3_f32 v198, v198, s20, v13
	v_med3_f32 v199, v199, s20, v13
	v_med3_f32 v200, v200, s20, v13
	v_med3_f32 v201, v201, s20, v13
	v_med3_f32 v202, v202, s20, v13
	v_med3_f32 v203, v203, s20, v13
	v_mov_b32_e32 v208, 0
	v_mov_b32_e32 v209, 0
	v_mov_b32_e32 v210, 0
	v_mov_b32_e32 v211, 0
	v_cvt_pk_fp8_f32 v208, v170, v171
	v_cvt_pk_fp8_f32 v209, v174, v175
	v_cvt_pk_fp8_f32 v210, v196, v197
	v_cvt_pk_fp8_f32 v211, v200, v201
	v_cvt_pk_fp8_f32 v208, v172, v173 op_sel:[0,0,1]
	v_cvt_pk_fp8_f32 v209, v176, v177 op_sel:[0,0,1]
	v_cvt_pk_fp8_f32 v210, v198, v199 op_sel:[0,0,1]
	v_cvt_pk_fp8_f32 v211, v202, v203 op_sel:[0,0,1]
	s_nop 0
	global_store_dwordx4 v12, v[208:211], s[14:15]
	s_waitcnt vmcnt(32)
	v_mul_f32_e32 v36, 0x43000000, v36
	v_mul_f32_e32 v37, 0x43000000, v37
	v_mul_f32_e32 v38, 0x43000000, v38
	v_mul_f32_e32 v39, 0x43000000, v39
	ds_write_b128 v4, v[36:39]
	v_mul_f32_e32 v40, 0x43000000, v40
	v_mul_f32_e32 v41, 0x43000000, v41
	v_mul_f32_e32 v42, 0x43000000, v42
	v_mul_f32_e32 v43, 0x43000000, v43
	ds_write_b128 v4, v[40:43] offset:1024
	v_mul_f32_e32 v44, 0x43000000, v44
	v_mul_f32_e32 v45, 0x43000000, v45
	v_mul_f32_e32 v46, 0x43000000, v46
	v_mul_f32_e32 v47, 0x43000000, v47
	ds_write_b128 v4, v[44:47] offset:2048
	v_mul_f32_e32 v48, 0x43000000, v48
	v_mul_f32_e32 v49, 0x43000000, v49
	v_mul_f32_e32 v50, 0x43000000, v50
	v_mul_f32_e32 v51, 0x43000000, v51
	ds_write_b128 v4, v[48:51] offset:3072
	v_mul_f32_e32 v52, 0x43000000, v52
	v_mul_f32_e32 v53, 0x43000000, v53
	v_mul_f32_e32 v54, 0x43000000, v54
	v_mul_f32_e32 v55, 0x43000000, v55
	ds_write_b128 v4, v[52:55] offset:4096
	v_mul_f32_e32 v56, 0x43000000, v56
	v_mul_f32_e32 v57, 0x43000000, v57
	v_mul_f32_e32 v58, 0x43000000, v58
	v_mul_f32_e32 v59, 0x43000000, v59
	ds_write_b128 v4, v[56:59] offset:5120
	v_mul_f32_e32 v60, 0x43000000, v60
	v_mul_f32_e32 v61, 0x43000000, v61
	v_mul_f32_e32 v62, 0x43000000, v62
	v_mul_f32_e32 v63, 0x43000000, v63
	ds_write_b128 v4, v[60:63] offset:6144
	v_mul_f32_e32 v64, 0x43000000, v64
	v_mul_f32_e32 v65, 0x43000000, v65
	v_mul_f32_e32 v66, 0x43000000, v66
	v_mul_f32_e32 v67, 0x43000000, v67
	ds_write_b128 v4, v[64:67] offset:7168
	s_waitcnt lgkmcnt(0)
	s_barrier
; #define GAS __attribute__((address_space(1)))
; #define LAS __attribute__((address_space(3)))
; #define LDS_WAIT() asm volatile("s_waitcnt lgkmcnt(0)" ::: "memory")
; __device__ __forceinline__ unsigned pk4_fp8(float a, float b, float c, float d) {
;     a = fminf(fmaxf(a, -448.f), 448.f); b = fminf(fmaxf(b, -448.f), 448.f); c = fminf(fmaxf(c, -448.f), 448.f); d = fminf(fmaxf(d, -448.f), 448.f);
;     int w = __builtin_amdgcn_cvt_pk_fp8_f32(a, b, 0, false); w = __builtin_amdgcn_cvt_pk_fp8_f32(c, d, w, true); return (unsigned)w; }
;     const int pr = item >> 1, kb = 2 * (pr / nblk) + (item & 1), nb = pr % nblk, k0 = 64 * kb, n0 = 32 * nb;
;     const int nr = n0 + (lane & 31); const int sc = MAP == 1 ? src_col_in(nr) : nr;
;     float v[32];
; #pragma unroll
;     for (int i = 0; i < 32; ++i) v[i] = sc >= 0 ? W[(size_t)(k0 + 2 * i + (lane >> 5)) * Nsrc + sc] : 0.f;
; #pragma unroll
;     for (int i = 0; i < 32; ++i) { const int k = k0 + 2 * i + (lane >> 5); float x = v[i] * wscale; if (KS) x *= (k < ksplit ? ksA[k] : ksB[k - ksplit]); scr[(2 * i + (lane >> 5)) * 33 + (lane & 31)] = x; }
;     LDS_WAIT(); asm volatile("" ::: "memory");
;     const int c = lane & 7;
; #pragma unroll
;     for (int j = 0; j < 4; ++j) { const int n = (lane >> 3) + 8 * j; const LAS float* s = scr + (8 * c) * 33 + n;
;         const unsigned long long o = (unsigned long long)pg8::pk4_fp8(s[0 * 33], s[1 * 33], s[2 * 33], s[3 * 33]) | ((unsigned long long)pg8::pk4_fp8(s[4 * 33], s[5 * 33], s[6 * 33], s[7 * 33]) << 32);
;         *(GAS unsigned long long*)(WT + (size_t)(n0 + n) * K + k0 + 8 * c) = o; }
;     LDS_WAIT(); asm volatile("" ::: "memory");
; }
	s_add_i32 s17, s16, 2304
	s_min_u32 s17, s17, 0xfff
	s_lshr_b32 s18, s17, 5
	s_add_i32 s18, s18, 0
	s_and_b32 s19, s17, 31
	s_lshl_b32 s18, s18, 21
	s_lshl_b32 s19, s19, 9
	s_add_u32 s18, s18, s19
	s_add_u32 s12, s2, s18
	s_addc_u32 s13, s3, 0
	global_load_dwordx4 v[36:39], v10, s[12:13]
	s_add_u32 s12, s12, 0x8000
	s_addc_u32 s13, s13, 0
	global_load_dwordx4 v[40:43], v10, s[12:13]
	s_add_u32 s12, s12, 0x8000
	s_addc_u32 s13, s13, 0
	global_load_dwordx4 v[44:47], v10, s[12:13]
	s_add_u32 s12, s12, 0x8000
	s_addc_u32 s13, s13, 0
	global_load_dwordx4 v[48:51], v10, s[12:13]
	s_add_u32 s12, s12, 0x8000
	s_addc_u32 s13, s13, 0
	global_load_dwordx4 v[52:55], v10, s[12:13]
	s_add_u32 s12, s12, 0x8000
	s_addc_u32 s13, s13, 0
	global_load_dwordx4 v[56:59], v10, s[12:13]
	s_add_u32 s12, s12, 0x8000
	s_addc_u32 s13, s13, 0
	global_load_dwordx4 v[60:63], v10, s[12:13]
	s_add_u32 s12, s12, 0x8000
	s_addc_u32 s13, s13, 0
	global_load_dwordx4 v[64:67], v10, s[12:13]
	s_add_i32 s17, s16, 1920
	s_min_u32 s17, s17, 0xfff
	s_lshr_b32 s18, s17, 5
	s_add_i32 s18, s18, 0
	s_and_b32 s19, s17, 31
	s_lshl_b32 s19, s19, 21
	s_lshl_b32 s18, s18, 7
	s_add_u32 s18, s18, s19
	s_add_u32 s14, s4, s18
	s_addc_u32 s15, s5, 0
	ds_read_b32 v170, v6
	ds_read_b32 v171, v6 offset:512
	ds_read_b32 v172, v6 offset:1024
	ds_read_b32 v173, v6 offset:1536
	ds_read_b32 v174, v6 offset:2048
	ds_read_b32 v175, v6 offset:2560
	ds_read_b32 v176, v6 offset:3072
	ds_read_b32 v177, v6 offset:3584
	ds_read_b32 v196, v6 offset:4096
	ds_read_b32 v197, v6 offset:4608
	ds_read_b32 v198, v6 offset:5120
	ds_read_b32 v199, v6 offset:5632
	ds_read_b32 v200, v6 offset:6144
	ds_read_b32 v201, v6 offset:6656
	ds_read_b32 v202, v6 offset:7168
	ds_read_b32 v203, v6 offset:7680
	s_waitcnt lgkmcnt(0)
	v_max_f32_e32 v170, v170, v170
	v_max_f32_e32 v171, v171, v171
	v_max_f32_e32 v172, v172, v172
	v_max_f32_e32 v173, v173, v173
	v_max_f32_e32 v174, v174, v174
	v_max_f32_e32 v175, v175, v175
	v_max_f32_e32 v176, v176, v176
	v_max_f32_e32 v177, v177, v177
	v_max_f32_e32 v196, v196, v196
	v_max_f32_e32 v197, v197, v197
	v_max_f32_e32 v198, v198, v198
	v_max_f32_e32 v199, v199, v199
	v_max_f32_e32 v200, v200, v200
	v_max_f32_e32 v201, v201, v201
	v_max_f32_e32 v202, v202, v202
	v_max_f32_e32 v203, v203, v203
	v_med3_f32 v170, v170, s20, v13
	v_med3_f32 v171, v171, s20, v13
	v_med3_f32 v172, v172, s20, v13
	v_med3_f32 v173, v173, s20, v13
	v_med3_f32 v174, v174, s20, v13
	v_med3_f32 v175, v175, s20, v13
	v_med3_f32 v176, v176, s20, v13
	v_med3_f32 v177, v177, s20, v13
	v_med3_f32 v196, v196, s20, v13
	v_med3_f32 v197, v197, s20, v13
	v_med3_f32 v198, v198, s20, v13
	v_med3_f32 v199, v199, s20, v13
	v_med3_f32 v200, v200, s20, v13
	v_med3_f32 v201, v201, s20, v13
	v_med3_f32 v202, v202, s20, v13
	v_med3_f32 v203, v203, s20, v13
	v_mov_b32_e32 v208, 0
	v_mov_b32_e32 v209, 0
	v_mov_b32_e32 v210, 0
	v_mov_b32_e32 v211, 0
	v_cvt_pk_fp8_f32 v208, v170, v171
	v_cvt_pk_fp8_f32 v209, v174, v175
	v_cvt_pk_fp8_f32 v210, v196, v197
	v_cvt_pk_fp8_f32 v211, v200, v201
	v_cvt_pk_fp8_f32 v208, v172, v173 op_sel:[0,0,1]
	v_cvt_pk_fp8_f32 v209, v176, v177 op_sel:[0,0,1]
	v_cvt_pk_fp8_f32 v210, v198, v199 op_sel:[0,0,1]
	v_cvt_pk_fp8_f32 v211, v202, v203 op_sel:[0,0,1]
	s_nop 0
	global_store_dwordx4 v11, v[208:211], s[14:15]
	ds_read_b32 v170, v8
	ds_read_b32 v171, v8 offset:512
	ds_read_b32 v172, v8 offset:1024
	ds_read_b32 v173, v8 offset:1536
	ds_read_b32 v174, v8 offset:2048
	ds_read_b32 v175, v8 offset:2560
	ds_read_b32 v176, v8 offset:3072
	ds_read_b32 v177, v8 offset:3584
	ds_read_b32 v196, v8 offset:4096
	ds_read_b32 v197, v8 offset:4608
	ds_read_b32 v198, v8 offset:5120
	ds_read_b32 v199, v8 offset:5632
	ds_read_b32 v200, v8 offset:6144
	ds_read_b32 v201, v8 offset:6656
	ds_read_b32 v202, v8 offset:7168
	ds_read_b32 v203, v8 offset:7680
	s_waitcnt lgkmcnt(0)
	v_max_f32_e32 v170, v170, v170
	v_max_f32_e32 v171, v171, v171
	v_max_f32_e32 v172, v172, v172
	v_max_f32_e32 v173, v173, v173
	v_max_f32_e32 v174, v174, v174
	v_max_f32_e32 v175, v175, v175
	v_max_f32_e32 v176, v176, v176
	v_max_f32_e32 v177, v177, v177
	v_max_f32_e32 v196, v196, v196
	v_max_f32_e32 v197, v197, v197
	v_max_f32_e32 v198, v198, v198
	v_max_f32_e32 v199, v199, v199
	v_max_f32_e32 v200, v200, v200
	v_max_f32_e32 v201, v201, v201
	v_max_f32_e32 v202, v202, v202
	v_max_f32_e32 v203, v203, v203
	v_med3_f32 v170, v170, s20, v13
	v_med3_f32 v171, v171, s20, v13
	v_med3_f32 v172, v172, s20, v13
	v_med3_f32 v173, v173, s20, v13
	v_med3_f32 v174, v174, s20, v13
	v_med3_f32 v175, v175, s20, v13
	v_med3_f32 v176, v176, s20, v13
	v_med3_f32 v177, v177, s20, v13
	v_med3_f32 v196, v196, s20, v13
	v_med3_f32 v197, v197, s20, v13
	v_med3_f32 v198, v198, s20, v13
	v_med3_f32 v199, v199, s20, v13
	v_med3_f32 v200, v200, s20, v13
	v_med3_f32 v201, v201, s20, v13
	v_med3_f32 v202, v202, s20, v13
	v_med3_f32 v203, v203, s20, v13
	v_mov_b32_e32 v208, 0
	v_mov_b32_e32 v209, 0
	v_mov_b32_e32 v210, 0
	v_mov_b32_e32 v211, 0
	v_cvt_pk_fp8_f32 v208, v170, v171
	v_cvt_pk_fp8_f32 v209, v174, v175
	v_cvt_pk_fp8_f32 v210, v196, v197
	v_cvt_pk_fp8_f32 v211, v200, v201
	v_cvt_pk_fp8_f32 v208, v172, v173 op_sel:[0,0,1]
	v_cvt_pk_fp8_f32 v209, v176, v177 op_sel:[0,0,1]
	v_cvt_pk_fp8_f32 v210, v198, v199 op_sel:[0,0,1]
	v_cvt_pk_fp8_f32 v211, v202, v203 op_sel:[0,0,1]
	s_nop 0
	global_store_dwordx4 v12, v[208:211], s[14:15]
	s_waitcnt vmcnt(32)
	v_mul_f32_e32 v68, 0x43000000, v68
	v_mul_f32_e32 v69, 0x43000000, v69
	v_mul_f32_e32 v70, 0x43000000, v70
	v_mul_f32_e32 v71, 0x43000000, v71
	ds_write_b128 v5, v[68:71]
	v_mul_f32_e32 v72, 0x43000000, v72
	v_mul_f32_e32 v73, 0x43000000, v73
	v_mul_f32_e32 v74, 0x43000000, v74
	v_mul_f32_e32 v75, 0x43000000, v75
	ds_write_b128 v5, v[72:75] offset:1024
	v_mul_f32_e32 v76, 0x43000000, v76
	v_mul_f32_e32 v77, 0x43000000, v77
	v_mul_f32_e32 v78, 0x43000000, v78
	v_mul_f32_e32 v79, 0x43000000, v79
	ds_write_b128 v5, v[76:79] offset:2048
	v_mul_f32_e32 v80, 0x43000000, v80
	v_mul_f32_e32 v81, 0x43000000, v81
	v_mul_f32_e32 v82, 0x43000000, v82
	v_mul_f32_e32 v83, 0x43000000, v83
	ds_write_b128 v5, v[80:83] offset:3072
	v_mul_f32_e32 v84, 0x43000000, v84
	v_mul_f32_e32 v85, 0x43000000, v85
	v_mul_f32_e32 v86, 0x43000000, v86
	v_mul_f32_e32 v87, 0x43000000, v87
	ds_write_b128 v5, v[84:87] offset:4096
	v_mul_f32_e32 v88, 0x43000000, v88
	v_mul_f32_e32 v89, 0x43000000, v89
	v_mul_f32_e32 v90, 0x43000000, v90
	v_mul_f32_e32 v91, 0x43000000, v91
	ds_write_b128 v5, v[88:91] offset:5120
	v_mul_f32_e32 v92, 0x43000000, v92
	v_mul_f32_e32 v93, 0x43000000, v93
	v_mul_f32_e32 v94, 0x43000000, v94
	v_mul_f32_e32 v95, 0x43000000, v95
	ds_write_b128 v5, v[92:95] offset:6144
	v_mul_f32_e32 v96, 0x43000000, v96
	v_mul_f32_e32 v97, 0x43000000, v97
	v_mul_f32_e32 v98, 0x43000000, v98
	v_mul_f32_e32 v99, 0x43000000, v99
	ds_write_b128 v5, v[96:99] offset:7168
	s_waitcnt lgkmcnt(0)
	s_barrier
; #define GAS __attribute__((address_space(1)))
; #define LAS __attribute__((address_space(3)))
; #define LDS_WAIT() asm volatile("s_waitcnt lgkmcnt(0)" ::: "memory")
; __device__ __forceinline__ unsigned pk4_fp8(float a, float b, float c, float d) {
;     a = fminf(fmaxf(a, -448.f), 448.f); b = fminf(fmaxf(b, -448.f), 448.f); c = fminf(fmaxf(c, -448.f), 448.f); d = fminf(fmaxf(d, -448.f), 448.f);
;     int w = __builtin_amdgcn_cvt_pk_fp8_f32(a, b, 0, false); w = __builtin_amdgcn_cvt_pk_fp8_f32(c, d, w, true); return (unsigned)w; }
;     ...
; #pragma unroll
;     for (int i = 0; i < 32; ++i) v[i] = sc >= 0 ? W[(size_t)(k0 + 2 * i + (lane >> 5)) * Nsrc + sc] : 0.f;
; #pragma unroll
;     for (int i = 0; i < 32; ++i) { const int k = k0 + 2 * i + (lane >> 5); float x = v[i] * wscale; if (KS) x *= (k < ksplit ? ksA[k] : ksB[k - ksplit]); scr[(2 * i + (lane >> 5)) * 33 + (lane & 31)] = x; }
;     LDS_WAIT(); asm volatile("" ::: "memory");
;     const int c = lane & 7;
; #pragma unroll
;     for (int j = 0; j < 4; ++j) { const int n = (lane >> 3) + 8 * j; const LAS float* s = scr + (8 * c) * 33 + n;
;         const unsigned long long o = (unsigned long long)pg8::pk4_fp8(s[0 * 33], s[1 * 33], s[2 * 33], s[3 * 33]) | ((unsigned long long)pg8::pk4_fp8(s[4 * 33], s[5 * 33], s[6 * 33], s[7 * 33]) << 32);
;         *(GAS unsigned long long*)(WT + (size_t)(n0 + n) * K + k0 + 8 * c) = o; }
	s_add_i32 s17, s16, 2400
	s_min_u32 s17, s17, 0xfff
	s_lshr_b32 s18, s17, 5
	s_add_i32 s18, s18, 0
	s_and_b32 s19, s17, 31
	s_lshl_b32 s18, s18, 21
	s_lshl_b32 s19, s19, 9
	s_add_u32 s18, s18, s19
	s_add_u32 s12, s2, s18
	s_addc_u32 s13, s3, 0
	global_load_dwordx4 v[68:71], v10, s[12:13]
	s_add_u32 s12, s12, 0x8000
	s_addc_u32 s13, s13, 0
	global_load_dwordx4 v[72:75], v10, s[12:13]
	s_add_u32 s12, s12, 0x8000
	s_addc_u32 s13, s13, 0
	global_load_dwordx4 v[76:79], v10, s[12:13]
	s_add_u32 s12, s12, 0x8000
	s_addc_u32 s13, s13, 0
	global_load_dwordx4 v[80:83], v10, s[12:13]
	s_add_u32 s12, s12, 0x8000
	s_addc_u32 s13, s13, 0
	global_load_dwordx4 v[84:87], v10, s[12:13]
	s_add_u32 s12, s12, 0x8000
	s_addc_u32 s13, s13, 0
	global_load_dwordx4 v[88:91], v10, s[12:13]
	s_add_u32 s12, s12, 0x8000
	s_addc_u32 s13, s13, 0
	global_load_dwordx4 v[92:95], v10, s[12:13]
	s_add_u32 s12, s12, 0x8000
	s_addc_u32 s13, s13, 0
	global_load_dwordx4 v[96:99], v10, s[12:13]
	s_add_i32 s17, s16, 2016
	s_min_u32 s17, s17, 0xfff
	s_lshr_b32 s18, s17, 5
	s_add_i32 s18, s18, 0
	s_and_b32 s19, s17, 31
	s_lshl_b32 s19, s19, 21
	s_lshl_b32 s18, s18, 7
	s_add_u32 s18, s18, s19
	s_add_u32 s14, s4, s18
	s_addc_u32 s15, s5, 0
	ds_read_b32 v170, v7
	ds_read_b32 v171, v7 offset:512
	ds_read_b32 v172, v7 offset:1024
	ds_read_b32 v173, v7 offset:1536
	ds_read_b32 v174, v7 offset:2048
	ds_read_b32 v175, v7 offset:2560
	ds_read_b32 v176, v7 offset:3072
	ds_read_b32 v177, v7 offset:3584
	ds_read_b32 v196, v7 offset:4096
	ds_read_b32 v197, v7 offset:4608
	ds_read_b32 v198, v7 offset:5120
	ds_read_b32 v199, v7 offset:5632
	ds_read_b32 v200, v7 offset:6144
	ds_read_b32 v201, v7 offset:6656
	ds_read_b32 v202, v7 offset:7168
	ds_read_b32 v203, v7 offset:7680
	s_waitcnt lgkmcnt(0)
	v_max_f32_e32 v170, v170, v170
	v_max_f32_e32 v171, v171, v171
	v_max_f32_e32 v172, v172, v172
	v_max_f32_e32 v173, v173, v173
	v_max_f32_e32 v174, v174, v174
	v_max_f32_e32 v175, v175, v175
	v_max_f32_e32 v176, v176, v176
	v_max_f32_e32 v177, v177, v177
	v_max_f32_e32 v196, v196, v196
	v_max_f32_e32 v197, v197, v197
	v_max_f32_e32 v198, v198, v198
	v_max_f32_e32 v199, v199, v199
	v_max_f32_e32 v200, v200, v200
	v_max_f32_e32 v201, v201, v201
	v_max_f32_e32 v202, v202, v202
	v_max_f32_e32 v203, v203, v203
	v_med3_f32 v170, v170, s20, v13
	v_med3_f32 v171, v171, s20, v13
	v_med3_f32 v172, v172, s20, v13
	v_med3_f32 v173, v173, s20, v13
	v_med3_f32 v174, v174, s20, v13
	v_med3_f32 v175, v175, s20, v13
	v_med3_f32 v176, v176, s20, v13
	v_med3_f32 v177, v177, s20, v13
	v_med3_f32 v196, v196, s20, v13
	v_med3_f32 v197, v197, s20, v13
	v_med3_f32 v198, v198, s20, v13
	v_med3_f32 v199, v199, s20, v13
	v_med3_f32 v200, v200, s20, v13
	v_med3_f32 v201, v201, s20, v13
	v_med3_f32 v202, v202, s20, v13
	v_med3_f32 v203, v203, s20, v13
	v_mov_b32_e32 v208, 0
	v_mov_b32_e32 v209, 0
	v_mov_b32_e32 v210, 0
	v_mov_b32_e32 v211, 0
	v_cvt_pk_fp8_f32 v208, v170, v171
	v_cvt_pk_fp8_f32 v209, v174, v175
	v_cvt_pk_fp8_f32 v210, v196, v197
	v_cvt_pk_fp8_f32 v211, v200, v201
	v_cvt_pk_fp8_f32 v208, v172, v173 op_sel:[0,0,1]
	v_cvt_pk_fp8_f32 v209, v176, v177 op_sel:[0,0,1]
	v_cvt_pk_fp8_f32 v210, v198, v199 op_sel:[0,0,1]
	v_cvt_pk_fp8_f32 v211, v202, v203 op_sel:[0,0,1]
	s_nop 0
	global_store_dwordx4 v11, v[208:211], s[14:15]
	ds_read_b32 v170, v9
	ds_read_b32 v171, v9 offset:512
	ds_read_b32 v172, v9 offset:1024
	ds_read_b32 v173, v9 offset:1536
	ds_read_b32 v174, v9 offset:2048
	ds_read_b32 v175, v9 offset:2560
	ds_read_b32 v176, v9 offset:3072
	ds_read_b32 v177, v9 offset:3584
	ds_read_b32 v196, v9 offset:4096
	ds_read_b32 v197, v9 offset:4608
	ds_read_b32 v198, v9 offset:5120
	ds_read_b32 v199, v9 offset:5632
	ds_read_b32 v200, v9 offset:6144
	ds_read_b32 v201, v9 offset:6656
	ds_read_b32 v202, v9 offset:7168
	ds_read_b32 v203, v9 offset:7680
	s_waitcnt lgkmcnt(0)
	v_max_f32_e32 v170, v170, v170
	v_max_f32_e32 v171, v171, v171
	v_max_f32_e32 v172, v172, v172
	v_max_f32_e32 v173, v173, v173
	v_max_f32_e32 v174, v174, v174
	v_max_f32_e32 v175, v175, v175
	v_max_f32_e32 v176, v176, v176
	v_max_f32_e32 v177, v177, v177
	v_max_f32_e32 v196, v196, v196
	v_max_f32_e32 v197, v197, v197
	v_max_f32_e32 v198, v198, v198
	v_max_f32_e32 v199, v199, v199
	v_max_f32_e32 v200, v200, v200
	v_max_f32_e32 v201, v201, v201
	v_max_f32_e32 v202, v202, v202
	v_max_f32_e32 v203, v203, v203
	v_med3_f32 v170, v170, s20, v13
	v_med3_f32 v171, v171, s20, v13
	v_med3_f32 v172, v172, s20, v13
	v_med3_f32 v173, v173, s20, v13
	v_med3_f32 v174, v174, s20, v13
	v_med3_f32 v175, v175, s20, v13
	v_med3_f32 v176, v176, s20, v13
	v_med3_f32 v177, v177, s20, v13
	v_med3_f32 v196, v196, s20, v13
	v_med3_f32 v197, v197, s20, v13
	v_med3_f32 v198, v198, s20, v13
	v_med3_f32 v199, v199, s20, v13
	v_med3_f32 v200, v200, s20, v13
	v_med3_f32 v201, v201, s20, v13
	v_med3_f32 v202, v202, s20, v13
	v_med3_f32 v203, v203, s20, v13
	v_mov_b32_e32 v208, 0
	v_mov_b32_e32 v209, 0
	v_mov_b32_e32 v210, 0
	v_mov_b32_e32 v211, 0
	v_cvt_pk_fp8_f32 v208, v170, v171
	v_cvt_pk_fp8_f32 v209, v174, v175
	v_cvt_pk_fp8_f32 v210, v196, v197
	v_cvt_pk_fp8_f32 v211, v200, v201
	v_cvt_pk_fp8_f32 v208, v172, v173 op_sel:[0,0,1]
	v_cvt_pk_fp8_f32 v209, v176, v177 op_sel:[0,0,1]
	v_cvt_pk_fp8_f32 v210, v198, v199 op_sel:[0,0,1]
	v_cvt_pk_fp8_f32 v211, v202, v203 op_sel:[0,0,1]
	s_nop 0
	global_store_dwordx4 v12, v[208:211], s[14:15]
	s_waitcnt vmcnt(32)
	v_mul_f32_e32 v100, 0x43000000, v100
	v_mul_f32_e32 v101, 0x43000000, v101
	v_mul_f32_e32 v102, 0x43000000, v102
	v_mul_f32_e32 v103, 0x43000000, v103
	ds_write_b128 v4, v[100:103]
	v_mul_f32_e32 v104, 0x43000000, v104
	v_mul_f32_e32 v105, 0x43000000, v105
	v_mul_f32_e32 v106, 0x43000000, v106
	v_mul_f32_e32 v107, 0x43000000, v107
	ds_write_b128 v4, v[104:107] offset:1024
	v_mul_f32_e32 v108, 0x43000000, v108
	v_mul_f32_e32 v109, 0x43000000, v109
	v_mul_f32_e32 v110, 0x43000000, v110
	v_mul_f32_e32 v111, 0x43000000, v111
	ds_write_b128 v4, v[108:111] offset:2048
	v_mul_f32_e32 v112, 0x43000000, v112
	v_mul_f32_e32 v113, 0x43000000, v113
	v_mul_f32_e32 v114, 0x43000000, v114
	v_mul_f32_e32 v115, 0x43000000, v115
	ds_write_b128 v4, v[112:115] offset:3072
	v_mul_f32_e32 v116, 0x43000000, v116
	v_mul_f32_e32 v117, 0x43000000, v117
	v_mul_f32_e32 v118, 0x43000000, v118
	v_mul_f32_e32 v119, 0x43000000, v119
	ds_write_b128 v4, v[116:119] offset:4096
	v_mul_f32_e32 v120, 0x43000000, v120
	v_mul_f32_e32 v121, 0x43000000, v121
	v_mul_f32_e32 v122, 0x43000000, v122
	v_mul_f32_e32 v123, 0x43000000, v123
	ds_write_b128 v4, v[120:123] offset:5120
	v_mul_f32_e32 v124, 0x43000000, v124
	v_mul_f32_e32 v125, 0x43000000, v125
	v_mul_f32_e32 v126, 0x43000000, v126
	v_mul_f32_e32 v127, 0x43000000, v127
	ds_write_b128 v4, v[124:127] offset:6144
	v_mul_f32_e32 v128, 0x43000000, v128
	v_mul_f32_e32 v129, 0x43000000, v129
	v_mul_f32_e32 v130, 0x43000000, v130
	v_mul_f32_e32 v131, 0x43000000, v131
	ds_write_b128 v4, v[128:131] offset:7168
	s_waitcnt lgkmcnt(0)
	s_barrier
; #define GAS __attribute__((address_space(1)))
; #define LAS __attribute__((address_space(3)))
; #define LDS_WAIT() asm volatile("s_waitcnt lgkmcnt(0)" ::: "memory")
; __device__ __forceinline__ unsigned pk4_fp8(float a, float b, float c, float d) {
;     a = fminf(fmaxf(a, -448.f), 448.f); b = fminf(fmaxf(b, -448.f), 448.f); c = fminf(fmaxf(c, -448.f), 448.f); d = fminf(fmaxf(d, -448.f), 448.f);
;     int w = __builtin_amdgcn_cvt_pk_fp8_f32(a, b, 0, false); w = __builtin_amdgcn_cvt_pk_fp8_f32(c, d, w, true); return (unsigned)w; }
;     ...
; #pragma unroll
;     for (int i = 0; i < 32; ++i) v[i] = sc >= 0 ? W[(size_t)(k0 + 2 * i + (lane >> 5)) * Nsrc + sc] : 0.f;
; #pragma unroll
;     for (int i = 0; i < 32; ++i) { const int k = k0 + 2 * i + (lane >> 5); float x = v[i] * wscale; if (KS) x *= (k < ksplit ? ksA[k] : ksB[k - ksplit]); scr[(2 * i + (lane >> 5)) * 33 + (lane & 31)] = x; }
;     LDS_WAIT(); asm volatile("" ::: "memory");
;     const int c = lane & 7;
; #pragma unroll
;     for (int j = 0; j < 4; ++j) { const int n = (lane >> 3) + 8 * j; const LAS float* s = scr + (8 * c) * 33 + n;
;         const unsigned long long o = (unsigned long long)pg8::pk4_fp8(s[0 * 33], s[1 * 33], s[2 * 33], s[3 * 33]) | ((unsigned long long)pg8::pk4_fp8(s[4 * 33], s[5 * 33], s[6 * 33], s[7 * 33]) << 32);
;         *(GAS unsigned long long*)(WT + (size_t)(n0 + n) * K + k0 + 8 * c) = o; }
	s_add_i32 s17, s16, 2496
	s_min_u32 s17, s17, 0xfff
	s_lshr_b32 s18, s17, 5
	s_add_i32 s18, s18, 0
	s_and_b32 s19, s17, 31
	s_lshl_b32 s18, s18, 21
	s_lshl_b32 s19, s19, 9
	s_add_u32 s18, s18, s19
	s_add_u32 s12, s2, s18
	s_addc_u32 s13, s3, 0
	global_load_dwordx4 v[100:103], v10, s[12:13]
	s_add_u32 s12, s12, 0x8000
	s_addc_u32 s13, s13, 0
	global_load_dwordx4 v[104:107], v10, s[12:13]
	s_add_u32 s12, s12, 0x8000
	s_addc_u32 s13, s13, 0
	global_load_dwordx4 v[108:111], v10, s[12:13]
	s_add_u32 s12, s12, 0x8000
	s_addc_u32 s13, s13, 0
	global_load_dwordx4 v[112:115], v10, s[12:13]
	s_add_u32 s12, s12, 0x8000
	s_addc_u32 s13, s13, 0
	global_load_dwordx4 v[116:119], v10, s[12:13]
	s_add_u32 s12, s12, 0x8000
	s_addc_u32 s13, s13, 0
	global_load_dwordx4 v[120:123], v10, s[12:13]
	s_add_u32 s12, s12, 0x8000
	s_addc_u32 s13, s13, 0
	global_load_dwordx4 v[124:127], v10, s[12:13]
	s_add_u32 s12, s12, 0x8000
	s_addc_u32 s13, s13, 0
	global_load_dwordx4 v[128:131], v10, s[12:13]
	s_add_i32 s17, s16, 2112
	s_min_u32 s17, s17, 0xfff
	s_lshr_b32 s18, s17, 5
	s_add_i32 s18, s18, 0
	s_and_b32 s19, s17, 31
	s_lshl_b32 s19, s19, 21
	s_lshl_b32 s18, s18, 7
	s_add_u32 s18, s18, s19
	s_add_u32 s14, s4, s18
	s_addc_u32 s15, s5, 0
	ds_read_b32 v170, v6
	ds_read_b32 v171, v6 offset:512
	ds_read_b32 v172, v6 offset:1024
	ds_read_b32 v173, v6 offset:1536
	ds_read_b32 v174, v6 offset:2048
	ds_read_b32 v175, v6 offset:2560
	ds_read_b32 v176, v6 offset:3072
	ds_read_b32 v177, v6 offset:3584
	ds_read_b32 v196, v6 offset:4096
	ds_read_b32 v197, v6 offset:4608
	ds_read_b32 v198, v6 offset:5120
	ds_read_b32 v199, v6 offset:5632
	ds_read_b32 v200, v6 offset:6144
	ds_read_b32 v201, v6 offset:6656
	ds_read_b32 v202, v6 offset:7168
	ds_read_b32 v203, v6 offset:7680
	s_waitcnt lgkmcnt(0)
	v_max_f32_e32 v170, v170, v170
	v_max_f32_e32 v171, v171, v171
	v_max_f32_e32 v172, v172, v172
	v_max_f32_e32 v173, v173, v173
	v_max_f32_e32 v174, v174, v174
	v_max_f32_e32 v175, v175, v175
	v_max_f32_e32 v176, v176, v176
	v_max_f32_e32 v177, v177, v177
	v_max_f32_e32 v196, v196, v196
	v_max_f32_e32 v197, v197, v197
	v_max_f32_e32 v198, v198, v198
	v_max_f32_e32 v199, v199, v199
	v_max_f32_e32 v200, v200, v200
	v_max_f32_e32 v201, v201, v201
	v_max_f32_e32 v202, v202, v202
	v_max_f32_e32 v203, v203, v203
	v_med3_f32 v170, v170, s20, v13
	v_med3_f32 v171, v171, s20, v13
	v_med3_f32 v172, v172, s20, v13
	v_med3_f32 v173, v173, s20, v13
	v_med3_f32 v174, v174, s20, v13
	v_med3_f32 v175, v175, s20, v13
	v_med3_f32 v176, v176, s20, v13
	v_med3_f32 v177, v177, s20, v13
	v_med3_f32 v196, v196, s20, v13
	v_med3_f32 v197, v197, s20, v13
	v_med3_f32 v198, v198, s20, v13
	v_med3_f32 v199, v199, s20, v13
	v_med3_f32 v200, v200, s20, v13
	v_med3_f32 v201, v201, s20, v13
	v_med3_f32 v202, v202, s20, v13
	v_med3_f32 v203, v203, s20, v13
	v_mov_b32_e32 v208, 0
	v_mov_b32_e32 v209, 0
	v_mov_b32_e32 v210, 0
	v_mov_b32_e32 v211, 0
	v_cvt_pk_fp8_f32 v208, v170, v171
	v_cvt_pk_fp8_f32 v209, v174, v175
	v_cvt_pk_fp8_f32 v210, v196, v197
	v_cvt_pk_fp8_f32 v211, v200, v201
	v_cvt_pk_fp8_f32 v208, v172, v173 op_sel:[0,0,1]
	v_cvt_pk_fp8_f32 v209, v176, v177 op_sel:[0,0,1]
	v_cvt_pk_fp8_f32 v210, v198, v199 op_sel:[0,0,1]
	v_cvt_pk_fp8_f32 v211, v202, v203 op_sel:[0,0,1]
	s_nop 0
	global_store_dwordx4 v11, v[208:211], s[14:15]
	ds_read_b32 v170, v8
	ds_read_b32 v171, v8 offset:512
	ds_read_b32 v172, v8 offset:1024
	ds_read_b32 v173, v8 offset:1536
	ds_read_b32 v174, v8 offset:2048
	ds_read_b32 v175, v8 offset:2560
	ds_read_b32 v176, v8 offset:3072
	ds_read_b32 v177, v8 offset:3584
	ds_read_b32 v196, v8 offset:4096
	ds_read_b32 v197, v8 offset:4608
	ds_read_b32 v198, v8 offset:5120
	ds_read_b32 v199, v8 offset:5632
	ds_read_b32 v200, v8 offset:6144
	ds_read_b32 v201, v8 offset:6656
	ds_read_b32 v202, v8 offset:7168
	ds_read_b32 v203, v8 offset:7680
	s_waitcnt lgkmcnt(0)
	v_max_f32_e32 v170, v170, v170
	v_max_f32_e32 v171, v171, v171
	v_max_f32_e32 v172, v172, v172
	v_max_f32_e32 v173, v173, v173
	v_max_f32_e32 v174, v174, v174
	v_max_f32_e32 v175, v175, v175
	v_max_f32_e32 v176, v176, v176
	v_max_f32_e32 v177, v177, v177
	v_max_f32_e32 v196, v196, v196
	v_max_f32_e32 v197, v197, v197
	v_max_f32_e32 v198, v198, v198
	v_max_f32_e32 v199, v199, v199
	v_max_f32_e32 v200, v200, v200
	v_max_f32_e32 v201, v201, v201
	v_max_f32_e32 v202, v202, v202
	v_max_f32_e32 v203, v203, v203
	v_med3_f32 v170, v170, s20, v13
	v_med3_f32 v171, v171, s20, v13
	v_med3_f32 v172, v172, s20, v13
	v_med3_f32 v173, v173, s20, v13
	v_med3_f32 v174, v174, s20, v13
	v_med3_f32 v175, v175, s20, v13
	v_med3_f32 v176, v176, s20, v13
	v_med3_f32 v177, v177, s20, v13
	v_med3_f32 v196, v196, s20, v13
	v_med3_f32 v197, v197, s20, v13
	v_med3_f32 v198, v198, s20, v13
	v_med3_f32 v199, v199, s20, v13
	v_med3_f32 v200, v200, s20, v13
	v_med3_f32 v201, v201, s20, v13
	v_med3_f32 v202, v202, s20, v13
	v_med3_f32 v203, v203, s20, v13
	v_mov_b32_e32 v208, 0
	v_mov_b32_e32 v209, 0
	v_mov_b32_e32 v210, 0
	v_mov_b32_e32 v211, 0
	v_cvt_pk_fp8_f32 v208, v170, v171
	v_cvt_pk_fp8_f32 v209, v174, v175
	v_cvt_pk_fp8_f32 v210, v196, v197
	v_cvt_pk_fp8_f32 v211, v200, v201
	v_cvt_pk_fp8_f32 v208, v172, v173 op_sel:[0,0,1]
	v_cvt_pk_fp8_f32 v209, v176, v177 op_sel:[0,0,1]
	v_cvt_pk_fp8_f32 v210, v198, v199 op_sel:[0,0,1]
	v_cvt_pk_fp8_f32 v211, v202, v203 op_sel:[0,0,1]
	s_nop 0
	global_store_dwordx4 v12, v[208:211], s[14:15]
	s_waitcnt vmcnt(32)
	v_mul_f32_e32 v132, 0x43000000, v132
	v_mul_f32_e32 v133, 0x43000000, v133
	v_mul_f32_e32 v134, 0x43000000, v134
	v_mul_f32_e32 v135, 0x43000000, v135
	ds_write_b128 v5, v[132:135]
	v_mul_f32_e32 v136, 0x43000000, v136
	v_mul_f32_e32 v137, 0x43000000, v137
	v_mul_f32_e32 v138, 0x43000000, v138
	v_mul_f32_e32 v139, 0x43000000, v139
	ds_write_b128 v5, v[136:139] offset:1024
	v_mul_f32_e32 v140, 0x43000000, v140
	v_mul_f32_e32 v141, 0x43000000, v141
	v_mul_f32_e32 v142, 0x43000000, v142
	v_mul_f32_e32 v143, 0x43000000, v143
	ds_write_b128 v5, v[140:143] offset:2048
	v_mul_f32_e32 v144, 0x43000000, v144
	v_mul_f32_e32 v145, 0x43000000, v145
	v_mul_f32_e32 v146, 0x43000000, v146
	v_mul_f32_e32 v147, 0x43000000, v147
	ds_write_b128 v5, v[144:147] offset:3072
	v_mul_f32_e32 v148, 0x43000000, v148
	v_mul_f32_e32 v149, 0x43000000, v149
	v_mul_f32_e32 v150, 0x43000000, v150
	v_mul_f32_e32 v151, 0x43000000, v151
	ds_write_b128 v5, v[148:151] offset:4096
	v_mul_f32_e32 v152, 0x43000000, v152
	v_mul_f32_e32 v153, 0x43000000, v153
	v_mul_f32_e32 v154, 0x43000000, v154
	v_mul_f32_e32 v155, 0x43000000, v155
	ds_write_b128 v5, v[152:155] offset:5120
	v_mul_f32_e32 v156, 0x43000000, v156
	v_mul_f32_e32 v157, 0x43000000, v157
	v_mul_f32_e32 v158, 0x43000000, v158
	v_mul_f32_e32 v159, 0x43000000, v159
	ds_write_b128 v5, v[156:159] offset:6144
	v_mul_f32_e32 v160, 0x43000000, v160
	v_mul_f32_e32 v161, 0x43000000, v161
	v_mul_f32_e32 v162, 0x43000000, v162
	v_mul_f32_e32 v163, 0x43000000, v163
	ds_write_b128 v5, v[160:163] offset:7168
	s_waitcnt lgkmcnt(0)
	s_barrier
; #define GAS __attribute__((address_space(1)))
; #define LAS __attribute__((address_space(3)))
; #define LDS_WAIT() asm volatile("s_waitcnt lgkmcnt(0)" ::: "memory")
; __device__ __forceinline__ unsigned pk4_fp8(float a, float b, float c, float d) {
;     a = fminf(fmaxf(a, -448.f), 448.f); b = fminf(fmaxf(b, -448.f), 448.f); c = fminf(fmaxf(c, -448.f), 448.f); d = fminf(fmaxf(d, -448.f), 448.f);
;     int w = __builtin_amdgcn_cvt_pk_fp8_f32(a, b, 0, false); w = __builtin_amdgcn_cvt_pk_fp8_f32(c, d, w, true); return (unsigned)w; }
;     ...
; #pragma unroll
;     for (int i = 0; i < 32; ++i) v[i] = sc >= 0 ? W[(size_t)(k0 + 2 * i + (lane >> 5)) * Nsrc + sc] : 0.f;
; #pragma unroll
;     for (int i = 0; i < 32; ++i) { const int k = k0 + 2 * i + (lane >> 5); float x = v[i] * wscale; if (KS) x *= (k < ksplit ? ksA[k] : ksB[k - ksplit]); scr[(2 * i + (lane >> 5)) * 33 + (lane & 31)] = x; }
;     LDS_WAIT(); asm volatile("" ::: "memory");
;     const int c = lane & 7;
; #pragma unroll
;     for (int j = 0; j < 4; ++j) { const int n = (lane >> 3) + 8 * j; const LAS float* s = scr + (8 * c) * 33 + n;
;         const unsigned long long o = (unsigned long long)pg8::pk4_fp8(s[0 * 33], s[1 * 33], s[2 * 33], s[3 * 33]) | ((unsigned long long)pg8::pk4_fp8(s[4 * 33], s[5 * 33], s[6 * 33], s[7 * 33]) << 32);
;         *(GAS unsigned long long*)(WT + (size_t)(n0 + n) * K + k0 + 8 * c) = o; }
	s_add_i32 s17, s16, 2592
	s_min_u32 s17, s17, 0xfff
	s_lshr_b32 s18, s17, 5
	s_add_i32 s18, s18, 0
	s_and_b32 s19, s17, 31
	s_lshl_b32 s18, s18, 21
	s_lshl_b32 s19, s19, 9
	s_add_u32 s18, s18, s19
	s_add_u32 s12, s2, s18
	s_addc_u32 s13, s3, 0
	global_load_dwordx4 v[132:135], v10, s[12:13]
	s_add_u32 s12, s12, 0x8000
	s_addc_u32 s13, s13, 0
	global_load_dwordx4 v[136:139], v10, s[12:13]
	s_add_u32 s12, s12, 0x8000
	s_addc_u32 s13, s13, 0
	global_load_dwordx4 v[140:143], v10, s[12:13]
	s_add_u32 s12, s12, 0x8000
	s_addc_u32 s13, s13, 0
	global_load_dwordx4 v[144:147], v10, s[12:13]
	s_add_u32 s12, s12, 0x8000
	s_addc_u32 s13, s13, 0
	global_load_dwordx4 v[148:151], v10, s[12:13]
	s_add_u32 s12, s12, 0x8000
	s_addc_u32 s13, s13, 0
	global_load_dwordx4 v[152:155], v10, s[12:13]
	s_add_u32 s12, s12, 0x8000
	s_addc_u32 s13, s13, 0
	global_load_dwordx4 v[156:159], v10, s[12:13]
	s_add_u32 s12, s12, 0x8000
	s_addc_u32 s13, s13, 0
	global_load_dwordx4 v[160:163], v10, s[12:13]
	s_add_i32 s17, s16, 2208
	s_min_u32 s17, s17, 0xfff
	s_lshr_b32 s18, s17, 5
	s_add_i32 s18, s18, 0
	s_and_b32 s19, s17, 31
	s_lshl_b32 s19, s19, 21
	s_lshl_b32 s18, s18, 7
	s_add_u32 s18, s18, s19
	s_add_u32 s14, s4, s18
	s_addc_u32 s15, s5, 0
	ds_read_b32 v170, v7
	ds_read_b32 v171, v7 offset:512
	ds_read_b32 v172, v7 offset:1024
	ds_read_b32 v173, v7 offset:1536
	ds_read_b32 v174, v7 offset:2048
	ds_read_b32 v175, v7 offset:2560
	ds_read_b32 v176, v7 offset:3072
	ds_read_b32 v177, v7 offset:3584
	ds_read_b32 v196, v7 offset:4096
	ds_read_b32 v197, v7 offset:4608
	ds_read_b32 v198, v7 offset:5120
	ds_read_b32 v199, v7 offset:5632
	ds_read_b32 v200, v7 offset:6144
	ds_read_b32 v201, v7 offset:6656
	ds_read_b32 v202, v7 offset:7168
	ds_read_b32 v203, v7 offset:7680
	s_waitcnt lgkmcnt(0)
	v_max_f32_e32 v170, v170, v170
	v_max_f32_e32 v171, v171, v171
	v_max_f32_e32 v172, v172, v172
	v_max_f32_e32 v173, v173, v173
	v_max_f32_e32 v174, v174, v174
	v_max_f32_e32 v175, v175, v175
	v_max_f32_e32 v176, v176, v176
	v_max_f32_e32 v177, v177, v177
	v_max_f32_e32 v196, v196, v196
	v_max_f32_e32 v197, v197, v197
	v_max_f32_e32 v198, v198, v198
	v_max_f32_e32 v199, v199, v199
	v_max_f32_e32 v200, v200, v200
	v_max_f32_e32 v201, v201, v201
	v_max_f32_e32 v202, v202, v202
	v_max_f32_e32 v203, v203, v203
	v_med3_f32 v170, v170, s20, v13
	v_med3_f32 v171, v171, s20, v13
	v_med3_f32 v172, v172, s20, v13
	v_med3_f32 v173, v173, s20, v13
	v_med3_f32 v174, v174, s20, v13
	v_med3_f32 v175, v175, s20, v13
	v_med3_f32 v176, v176, s20, v13
	v_med3_f32 v177, v177, s20, v13
	v_med3_f32 v196, v196, s20, v13
	v_med3_f32 v197, v197, s20, v13
	v_med3_f32 v198, v198, s20, v13
	v_med3_f32 v199, v199, s20, v13
	v_med3_f32 v200, v200, s20, v13
	v_med3_f32 v201, v201, s20, v13
	v_med3_f32 v202, v202, s20, v13
	v_med3_f32 v203, v203, s20, v13
	v_mov_b32_e32 v208, 0
	v_mov_b32_e32 v209, 0
	v_mov_b32_e32 v210, 0
	v_mov_b32_e32 v211, 0
	v_cvt_pk_fp8_f32 v208, v170, v171
	v_cvt_pk_fp8_f32 v209, v174, v175
	v_cvt_pk_fp8_f32 v210, v196, v197
	v_cvt_pk_fp8_f32 v211, v200, v201
	v_cvt_pk_fp8_f32 v208, v172, v173 op_sel:[0,0,1]
	v_cvt_pk_fp8_f32 v209, v176, v177 op_sel:[0,0,1]
	v_cvt_pk_fp8_f32 v210, v198, v199 op_sel:[0,0,1]
	v_cvt_pk_fp8_f32 v211, v202, v203 op_sel:[0,0,1]
	s_nop 0
	global_store_dwordx4 v11, v[208:211], s[14:15]
	ds_read_b32 v170, v9
	ds_read_b32 v171, v9 offset:512
	ds_read_b32 v172, v9 offset:1024
	ds_read_b32 v173, v9 offset:1536
	ds_read_b32 v174, v9 offset:2048
	ds_read_b32 v175, v9 offset:2560
	ds_read_b32 v176, v9 offset:3072
	ds_read_b32 v177, v9 offset:3584
	ds_read_b32 v196, v9 offset:4096
	ds_read_b32 v197, v9 offset:4608
	ds_read_b32 v198, v9 offset:5120
	ds_read_b32 v199, v9 offset:5632
	ds_read_b32 v200, v9 offset:6144
	ds_read_b32 v201, v9 offset:6656
	ds_read_b32 v202, v9 offset:7168
	ds_read_b32 v203, v9 offset:7680
	s_waitcnt lgkmcnt(0)
	v_max_f32_e32 v170, v170, v170
	v_max_f32_e32 v171, v171, v171
	v_max_f32_e32 v172, v172, v172
	v_max_f32_e32 v173, v173, v173
	v_max_f32_e32 v174, v174, v174
	v_max_f32_e32 v175, v175, v175
	v_max_f32_e32 v176, v176, v176
	v_max_f32_e32 v177, v177, v177
	v_max_f32_e32 v196, v196, v196
	v_max_f32_e32 v197, v197, v197
	v_max_f32_e32 v198, v198, v198
	v_max_f32_e32 v199, v199, v199
	v_max_f32_e32 v200, v200, v200
	v_max_f32_e32 v201, v201, v201
	v_max_f32_e32 v202, v202, v202
	v_max_f32_e32 v203, v203, v203
	v_med3_f32 v170, v170, s20, v13
	v_med3_f32 v171, v171, s20, v13
	v_med3_f32 v172, v172, s20, v13
	v_med3_f32 v173, v173, s20, v13
	v_med3_f32 v174, v174, s20, v13
	v_med3_f32 v175, v175, s20, v13
	v_med3_f32 v176, v176, s20, v13
	v_med3_f32 v177, v177, s20, v13
	v_med3_f32 v196, v196, s20, v13
	v_med3_f32 v197, v197, s20, v13
	v_med3_f32 v198, v198, s20, v13
	v_med3_f32 v199, v199, s20, v13
	v_med3_f32 v200, v200, s20, v13
	v_med3_f32 v201, v201, s20, v13
	v_med3_f32 v202, v202, s20, v13
	v_med3_f32 v203, v203, s20, v13
	v_mov_b32_e32 v208, 0
	v_mov_b32_e32 v209, 0
	v_mov_b32_e32 v210, 0
	v_mov_b32_e32 v211, 0
	v_cvt_pk_fp8_f32 v208, v170, v171
	v_cvt_pk_fp8_f32 v209, v174, v175
	v_cvt_pk_fp8_f32 v210, v196, v197
	v_cvt_pk_fp8_f32 v211, v200, v201
	v_cvt_pk_fp8_f32 v208, v172, v173 op_sel:[0,0,1]
	v_cvt_pk_fp8_f32 v209, v176, v177 op_sel:[0,0,1]
	v_cvt_pk_fp8_f32 v210, v198, v199 op_sel:[0,0,1]
	v_cvt_pk_fp8_f32 v211, v202, v203 op_sel:[0,0,1]
	s_nop 0
	global_store_dwordx4 v12, v[208:211], s[14:15]
	s_waitcnt vmcnt(32)
	v_mul_f32_e32 v36, 0x43000000, v36
	v_mul_f32_e32 v37, 0x43000000, v37
	v_mul_f32_e32 v38, 0x43000000, v38
	v_mul_f32_e32 v39, 0x43000000, v39
	ds_write_b128 v4, v[36:39]
	v_mul_f32_e32 v40, 0x43000000, v40
	v_mul_f32_e32 v41, 0x43000000, v41
	v_mul_f32_e32 v42, 0x43000000, v42
	v_mul_f32_e32 v43, 0x43000000, v43
	ds_write_b128 v4, v[40:43] offset:1024
	v_mul_f32_e32 v44, 0x43000000, v44
	v_mul_f32_e32 v45, 0x43000000, v45
	v_mul_f32_e32 v46, 0x43000000, v46
	v_mul_f32_e32 v47, 0x43000000, v47
	ds_write_b128 v4, v[44:47] offset:2048
	v_mul_f32_e32 v48, 0x43000000, v48
	v_mul_f32_e32 v49, 0x43000000, v49
	v_mul_f32_e32 v50, 0x43000000, v50
	v_mul_f32_e32 v51, 0x43000000, v51
	ds_write_b128 v4, v[48:51] offset:3072
	v_mul_f32_e32 v52, 0x43000000, v52
	v_mul_f32_e32 v53, 0x43000000, v53
	v_mul_f32_e32 v54, 0x43000000, v54
	v_mul_f32_e32 v55, 0x43000000, v55
	ds_write_b128 v4, v[52:55] offset:4096
	v_mul_f32_e32 v56, 0x43000000, v56
	v_mul_f32_e32 v57, 0x43000000, v57
	v_mul_f32_e32 v58, 0x43000000, v58
	v_mul_f32_e32 v59, 0x43000000, v59
	ds_write_b128 v4, v[56:59] offset:5120
	v_mul_f32_e32 v60, 0x43000000, v60
	v_mul_f32_e32 v61, 0x43000000, v61
	v_mul_f32_e32 v62, 0x43000000, v62
	v_mul_f32_e32 v63, 0x43000000, v63
	ds_write_b128 v4, v[60:63] offset:6144
	v_mul_f32_e32 v64, 0x43000000, v64
	v_mul_f32_e32 v65, 0x43000000, v65
	v_mul_f32_e32 v66, 0x43000000, v66
	v_mul_f32_e32 v67, 0x43000000, v67
	ds_write_b128 v4, v[64:67] offset:7168
	s_waitcnt lgkmcnt(0)
	s_barrier
; #define GAS __attribute__((address_space(1)))
; #define LAS __attribute__((address_space(3)))
; #define LDS_WAIT() asm volatile("s_waitcnt lgkmcnt(0)" ::: "memory")
; __device__ __forceinline__ unsigned pk4_fp8(float a, float b, float c, float d) {
;     a = fminf(fmaxf(a, -448.f), 448.f); b = fminf(fmaxf(b, -448.f), 448.f); c = fminf(fmaxf(c, -448.f), 448.f); d = fminf(fmaxf(d, -448.f), 448.f);
;     int w = __builtin_amdgcn_cvt_pk_fp8_f32(a, b, 0, false); w = __builtin_amdgcn_cvt_pk_fp8_f32(c, d, w, true); return (unsigned)w; }
;     ...
; #pragma unroll
;     for (int i = 0; i < 32; ++i) v[i] = sc >= 0 ? W[(size_t)(k0 + 2 * i + (lane >> 5)) * Nsrc + sc] : 0.f;
; #pragma unroll
;     for (int i = 0; i < 32; ++i) { const int k = k0 + 2 * i + (lane >> 5); float x = v[i] * wscale; if (KS) x *= (k < ksplit ? ksA[k] : ksB[k - ksplit]); scr[(2 * i + (lane >> 5)) * 33 + (lane & 31)] = x; }
;     LDS_WAIT(); asm volatile("" ::: "memory");
;     const int c = lane & 7;
; #pragma unroll
;     for (int j = 0; j < 4; ++j) { const int n = (lane >> 3) + 8 * j; const LAS float* s = scr + (8 * c) * 33 + n;
;         const unsigned long long o = (unsigned long long)pg8::pk4_fp8(s[0 * 33], s[1 * 33], s[2 * 33], s[3 * 33]) | ((unsigned long long)pg8::pk4_fp8(s[4 * 33], s[5 * 33], s[6 * 33], s[7 * 33]) << 32);
;         *(GAS unsigned long long*)(WT + (size_t)(n0 + n) * K + k0 + 8 * c) = o; }
	s_add_i32 s17, s16, 2688
	s_min_u32 s17, s17, 0xfff
	s_lshr_b32 s18, s17, 5
	s_add_i32 s18, s18, 0
	s_and_b32 s19, s17, 31
	s_lshl_b32 s18, s18, 21
	s_lshl_b32 s19, s19, 9
	s_add_u32 s18, s18, s19
	s_add_u32 s12, s2, s18
	s_addc_u32 s13, s3, 0
	global_load_dwordx4 v[36:39], v10, s[12:13]
	s_add_u32 s12, s12, 0x8000
	s_addc_u32 s13, s13, 0
	global_load_dwordx4 v[40:43], v10, s[12:13]
	s_add_u32 s12, s12, 0x8000
	s_addc_u32 s13, s13, 0
	global_load_dwordx4 v[44:47], v10, s[12:13]
	s_add_u32 s12, s12, 0x8000
	s_addc_u32 s13, s13, 0
	global_load_dwordx4 v[48:51], v10, s[12:13]
	s_add_u32 s12, s12, 0x8000
	s_addc_u32 s13, s13, 0
	global_load_dwordx4 v[52:55], v10, s[12:13]
	s_add_u32 s12, s12, 0x8000
	s_addc_u32 s13, s13, 0
	global_load_dwordx4 v[56:59], v10, s[12:13]
	s_add_u32 s12, s12, 0x8000
	s_addc_u32 s13, s13, 0
	global_load_dwordx4 v[60:63], v10, s[12:13]
	s_add_u32 s12, s12, 0x8000
	s_addc_u32 s13, s13, 0
	global_load_dwordx4 v[64:67], v10, s[12:13]
	s_add_i32 s17, s16, 2304
	s_min_u32 s17, s17, 0xfff
	s_lshr_b32 s18, s17, 5
	s_add_i32 s18, s18, 0
	s_and_b32 s19, s17, 31
	s_lshl_b32 s19, s19, 21
	s_lshl_b32 s18, s18, 7
	s_add_u32 s18, s18, s19
	s_add_u32 s14, s4, s18
	s_addc_u32 s15, s5, 0
	ds_read_b32 v170, v6
	ds_read_b32 v171, v6 offset:512
	ds_read_b32 v172, v6 offset:1024
	ds_read_b32 v173, v6 offset:1536
	ds_read_b32 v174, v6 offset:2048
	ds_read_b32 v175, v6 offset:2560
	ds_read_b32 v176, v6 offset:3072
	ds_read_b32 v177, v6 offset:3584
	ds_read_b32 v196, v6 offset:4096
	ds_read_b32 v197, v6 offset:4608
	ds_read_b32 v198, v6 offset:5120
	ds_read_b32 v199, v6 offset:5632
	ds_read_b32 v200, v6 offset:6144
	ds_read_b32 v201, v6 offset:6656
	ds_read_b32 v202, v6 offset:7168
	ds_read_b32 v203, v6 offset:7680
	s_waitcnt lgkmcnt(0)
	v_max_f32_e32 v170, v170, v170
	v_max_f32_e32 v171, v171, v171
	v_max_f32_e32 v172, v172, v172
	v_max_f32_e32 v173, v173, v173
	v_max_f32_e32 v174, v174, v174
	v_max_f32_e32 v175, v175, v175
	v_max_f32_e32 v176, v176, v176
	v_max_f32_e32 v177, v177, v177
	v_max_f32_e32 v196, v196, v196
	v_max_f32_e32 v197, v197, v197
	v_max_f32_e32 v198, v198, v198
	v_max_f32_e32 v199, v199, v199
	v_max_f32_e32 v200, v200, v200
	v_max_f32_e32 v201, v201, v201
	v_max_f32_e32 v202, v202, v202
	v_max_f32_e32 v203, v203, v203
	v_med3_f32 v170, v170, s20, v13
	v_med3_f32 v171, v171, s20, v13
	v_med3_f32 v172, v172, s20, v13
	v_med3_f32 v173, v173, s20, v13
	v_med3_f32 v174, v174, s20, v13
	v_med3_f32 v175, v175, s20, v13
	v_med3_f32 v176, v176, s20, v13
	v_med3_f32 v177, v177, s20, v13
	v_med3_f32 v196, v196, s20, v13
	v_med3_f32 v197, v197, s20, v13
	v_med3_f32 v198, v198, s20, v13
	v_med3_f32 v199, v199, s20, v13
	v_med3_f32 v200, v200, s20, v13
	v_med3_f32 v201, v201, s20, v13
	v_med3_f32 v202, v202, s20, v13
	v_med3_f32 v203, v203, s20, v13
	v_mov_b32_e32 v208, 0
	v_mov_b32_e32 v209, 0
	v_mov_b32_e32 v210, 0
	v_mov_b32_e32 v211, 0
	v_cvt_pk_fp8_f32 v208, v170, v171
	v_cvt_pk_fp8_f32 v209, v174, v175
	v_cvt_pk_fp8_f32 v210, v196, v197
	v_cvt_pk_fp8_f32 v211, v200, v201
	v_cvt_pk_fp8_f32 v208, v172, v173 op_sel:[0,0,1]
	v_cvt_pk_fp8_f32 v209, v176, v177 op_sel:[0,0,1]
	v_cvt_pk_fp8_f32 v210, v198, v199 op_sel:[0,0,1]
	v_cvt_pk_fp8_f32 v211, v202, v203 op_sel:[0,0,1]
	s_nop 0
	global_store_dwordx4 v11, v[208:211], s[14:15]
	ds_read_b32 v170, v8
	ds_read_b32 v171, v8 offset:512
	ds_read_b32 v172, v8 offset:1024
	ds_read_b32 v173, v8 offset:1536
	ds_read_b32 v174, v8 offset:2048
	ds_read_b32 v175, v8 offset:2560
	ds_read_b32 v176, v8 offset:3072
	ds_read_b32 v177, v8 offset:3584
	ds_read_b32 v196, v8 offset:4096
	ds_read_b32 v197, v8 offset:4608
	ds_read_b32 v198, v8 offset:5120
	ds_read_b32 v199, v8 offset:5632
	ds_read_b32 v200, v8 offset:6144
	ds_read_b32 v201, v8 offset:6656
	ds_read_b32 v202, v8 offset:7168
	ds_read_b32 v203, v8 offset:7680
	s_waitcnt lgkmcnt(0)
	v_max_f32_e32 v170, v170, v170
	v_max_f32_e32 v171, v171, v171
	v_max_f32_e32 v172, v172, v172
	v_max_f32_e32 v173, v173, v173
	v_max_f32_e32 v174, v174, v174
	v_max_f32_e32 v175, v175, v175
	v_max_f32_e32 v176, v176, v176
	v_max_f32_e32 v177, v177, v177
	v_max_f32_e32 v196, v196, v196
	v_max_f32_e32 v197, v197, v197
	v_max_f32_e32 v198, v198, v198
	v_max_f32_e32 v199, v199, v199
	v_max_f32_e32 v200, v200, v200
	v_max_f32_e32 v201, v201, v201
	v_max_f32_e32 v202, v202, v202
	v_max_f32_e32 v203, v203, v203
	v_med3_f32 v170, v170, s20, v13
	v_med3_f32 v171, v171, s20, v13
	v_med3_f32 v172, v172, s20, v13
	v_med3_f32 v173, v173, s20, v13
	v_med3_f32 v174, v174, s20, v13
	v_med3_f32 v175, v175, s20, v13
	v_med3_f32 v176, v176, s20, v13
	v_med3_f32 v177, v177, s20, v13
	v_med3_f32 v196, v196, s20, v13
	v_med3_f32 v197, v197, s20, v13
	v_med3_f32 v198, v198, s20, v13
	v_med3_f32 v199, v199, s20, v13
	v_med3_f32 v200, v200, s20, v13
	v_med3_f32 v201, v201, s20, v13
	v_med3_f32 v202, v202, s20, v13
	v_med3_f32 v203, v203, s20, v13
	v_mov_b32_e32 v208, 0
	v_mov_b32_e32 v209, 0
	v_mov_b32_e32 v210, 0
	v_mov_b32_e32 v211, 0
	v_cvt_pk_fp8_f32 v208, v170, v171
	v_cvt_pk_fp8_f32 v209, v174, v175
	v_cvt_pk_fp8_f32 v210, v196, v197
	v_cvt_pk_fp8_f32 v211, v200, v201
	v_cvt_pk_fp8_f32 v208, v172, v173 op_sel:[0,0,1]
	v_cvt_pk_fp8_f32 v209, v176, v177 op_sel:[0,0,1]
	v_cvt_pk_fp8_f32 v210, v198, v199 op_sel:[0,0,1]
	v_cvt_pk_fp8_f32 v211, v202, v203 op_sel:[0,0,1]
	s_nop 0
	global_store_dwordx4 v12, v[208:211], s[14:15]
	s_waitcnt vmcnt(32)
	v_mul_f32_e32 v68, 0x43000000, v68
	v_mul_f32_e32 v69, 0x43000000, v69
	v_mul_f32_e32 v70, 0x43000000, v70
	v_mul_f32_e32 v71, 0x43000000, v71
	ds_write_b128 v5, v[68:71]
	v_mul_f32_e32 v72, 0x43000000, v72
	v_mul_f32_e32 v73, 0x43000000, v73
	v_mul_f32_e32 v74, 0x43000000, v74
	v_mul_f32_e32 v75, 0x43000000, v75
	ds_write_b128 v5, v[72:75] offset:1024
	v_mul_f32_e32 v76, 0x43000000, v76
	v_mul_f32_e32 v77, 0x43000000, v77
	v_mul_f32_e32 v78, 0x43000000, v78
	v_mul_f32_e32 v79, 0x43000000, v79
	ds_write_b128 v5, v[76:79] offset:2048
	v_mul_f32_e32 v80, 0x43000000, v80
	v_mul_f32_e32 v81, 0x43000000, v81
	v_mul_f32_e32 v82, 0x43000000, v82
	v_mul_f32_e32 v83, 0x43000000, v83
	ds_write_b128 v5, v[80:83] offset:3072
	v_mul_f32_e32 v84, 0x43000000, v84
	v_mul_f32_e32 v85, 0x43000000, v85
	v_mul_f32_e32 v86, 0x43000000, v86
	v_mul_f32_e32 v87, 0x43000000, v87
	ds_write_b128 v5, v[84:87] offset:4096
	v_mul_f32_e32 v88, 0x43000000, v88
	v_mul_f32_e32 v89, 0x43000000, v89
	v_mul_f32_e32 v90, 0x43000000, v90
	v_mul_f32_e32 v91, 0x43000000, v91
	ds_write_b128 v5, v[88:91] offset:5120
	v_mul_f32_e32 v92, 0x43000000, v92
	v_mul_f32_e32 v93, 0x43000000, v93
	v_mul_f32_e32 v94, 0x43000000, v94
	v_mul_f32_e32 v95, 0x43000000, v95
	ds_write_b128 v5, v[92:95] offset:6144
	v_mul_f32_e32 v96, 0x43000000, v96
	v_mul_f32_e32 v97, 0x43000000, v97
	v_mul_f32_e32 v98, 0x43000000, v98
	v_mul_f32_e32 v99, 0x43000000, v99
	ds_write_b128 v5, v[96:99] offset:7168
	s_waitcnt lgkmcnt(0)
	s_barrier
; #define GAS __attribute__((address_space(1)))
; #define LAS __attribute__((address_space(3)))
; #define LDS_WAIT() asm volatile("s_waitcnt lgkmcnt(0)" ::: "memory")
; __device__ __forceinline__ unsigned pk4_fp8(float a, float b, float c, float d) {
;     a = fminf(fmaxf(a, -448.f), 448.f); b = fminf(fmaxf(b, -448.f), 448.f); c = fminf(fmaxf(c, -448.f), 448.f); d = fminf(fmaxf(d, -448.f), 448.f);
;     int w = __builtin_amdgcn_cvt_pk_fp8_f32(a, b, 0, false); w = __builtin_amdgcn_cvt_pk_fp8_f32(c, d, w, true); return (unsigned)w; }
;     ...
; #pragma unroll
;     for (int i = 0; i < 32; ++i) v[i] = sc >= 0 ? W[(size_t)(k0 + 2 * i + (lane >> 5)) * Nsrc + sc] : 0.f;
; #pragma unroll
;     for (int i = 0; i < 32; ++i) { const int k = k0 + 2 * i + (lane >> 5); float x = v[i] * wscale; if (KS) x *= (k < ksplit ? ksA[k] : ksB[k - ksplit]); scr[(2 * i + (lane >> 5)) * 33 + (lane & 31)] = x; }
;     LDS_WAIT(); asm volatile("" ::: "memory");
;     const int c = lane & 7;
; #pragma unroll
;     for (int j = 0; j < 4; ++j) { const int n = (lane >> 3) + 8 * j; const LAS float* s = scr + (8 * c) * 33 + n;
;         const unsigned long long o = (unsigned long long)pg8::pk4_fp8(s[0 * 33], s[1 * 33], s[2 * 33], s[3 * 33]) | ((unsigned long long)pg8::pk4_fp8(s[4 * 33], s[5 * 33], s[6 * 33], s[7 * 33]) << 32);
;         *(GAS unsigned long long*)(WT + (size_t)(n0 + n) * K + k0 + 8 * c) = o; }
	s_add_i32 s17, s16, 2784
	s_min_u32 s17, s17, 0xfff
	s_lshr_b32 s18, s17, 5
	s_add_i32 s18, s18, 0
	s_and_b32 s19, s17, 31
	s_lshl_b32 s18, s18, 21
	s_lshl_b32 s19, s19, 9
	s_add_u32 s18, s18, s19
	s_add_u32 s12, s2, s18
	s_addc_u32 s13, s3, 0
	global_load_dwordx4 v[68:71], v10, s[12:13]
	s_add_u32 s12, s12, 0x8000
	s_addc_u32 s13, s13, 0
	global_load_dwordx4 v[72:75], v10, s[12:13]
	s_add_u32 s12, s12, 0x8000
	s_addc_u32 s13, s13, 0
	global_load_dwordx4 v[76:79], v10, s[12:13]
	s_add_u32 s12, s12, 0x8000
	s_addc_u32 s13, s13, 0
	global_load_dwordx4 v[80:83], v10, s[12:13]
	s_add_u32 s12, s12, 0x8000
	s_addc_u32 s13, s13, 0
	global_load_dwordx4 v[84:87], v10, s[12:13]
	s_add_u32 s12, s12, 0x8000
	s_addc_u32 s13, s13, 0
	global_load_dwordx4 v[88:91], v10, s[12:13]
	s_add_u32 s12, s12, 0x8000
	s_addc_u32 s13, s13, 0
	global_load_dwordx4 v[92:95], v10, s[12:13]
	s_add_u32 s12, s12, 0x8000
	s_addc_u32 s13, s13, 0
	global_load_dwordx4 v[96:99], v10, s[12:13]
	s_add_i32 s17, s16, 2400
	s_min_u32 s17, s17, 0xfff
	s_lshr_b32 s18, s17, 5
	s_add_i32 s18, s18, 0
	s_and_b32 s19, s17, 31
	s_lshl_b32 s19, s19, 21
	s_lshl_b32 s18, s18, 7
	s_add_u32 s18, s18, s19
	s_add_u32 s14, s4, s18
	s_addc_u32 s15, s5, 0
	ds_read_b32 v170, v7
	ds_read_b32 v171, v7 offset:512
	ds_read_b32 v172, v7 offset:1024
	ds_read_b32 v173, v7 offset:1536
	ds_read_b32 v174, v7 offset:2048
	ds_read_b32 v175, v7 offset:2560
	ds_read_b32 v176, v7 offset:3072
	ds_read_b32 v177, v7 offset:3584
	ds_read_b32 v196, v7 offset:4096
	ds_read_b32 v197, v7 offset:4608
	ds_read_b32 v198, v7 offset:5120
	ds_read_b32 v199, v7 offset:5632
	ds_read_b32 v200, v7 offset:6144
	ds_read_b32 v201, v7 offset:6656
	ds_read_b32 v202, v7 offset:7168
	ds_read_b32 v203, v7 offset:7680
	s_waitcnt lgkmcnt(0)
	v_max_f32_e32 v170, v170, v170
	v_max_f32_e32 v171, v171, v171
	v_max_f32_e32 v172, v172, v172
	v_max_f32_e32 v173, v173, v173
	v_max_f32_e32 v174, v174, v174
	v_max_f32_e32 v175, v175, v175
	v_max_f32_e32 v176, v176, v176
	v_max_f32_e32 v177, v177, v177
	v_max_f32_e32 v196, v196, v196
	v_max_f32_e32 v197, v197, v197
	v_max_f32_e32 v198, v198, v198
	v_max_f32_e32 v199, v199, v199
	v_max_f32_e32 v200, v200, v200
	v_max_f32_e32 v201, v201, v201
	v_max_f32_e32 v202, v202, v202
	v_max_f32_e32 v203, v203, v203
	v_med3_f32 v170, v170, s20, v13
	v_med3_f32 v171, v171, s20, v13
	v_med3_f32 v172, v172, s20, v13
	v_med3_f32 v173, v173, s20, v13
	v_med3_f32 v174, v174, s20, v13
	v_med3_f32 v175, v175, s20, v13
	v_med3_f32 v176, v176, s20, v13
	v_med3_f32 v177, v177, s20, v13
	v_med3_f32 v196, v196, s20, v13
	v_med3_f32 v197, v197, s20, v13
	v_med3_f32 v198, v198, s20, v13
	v_med3_f32 v199, v199, s20, v13
	v_med3_f32 v200, v200, s20, v13
	v_med3_f32 v201, v201, s20, v13
	v_med3_f32 v202, v202, s20, v13
	v_med3_f32 v203, v203, s20, v13
	v_mov_b32_e32 v208, 0
	v_mov_b32_e32 v209, 0
	v_mov_b32_e32 v210, 0
	v_mov_b32_e32 v211, 0
	v_cvt_pk_fp8_f32 v208, v170, v171
	v_cvt_pk_fp8_f32 v209, v174, v175
	v_cvt_pk_fp8_f32 v210, v196, v197
	v_cvt_pk_fp8_f32 v211, v200, v201
	v_cvt_pk_fp8_f32 v208, v172, v173 op_sel:[0,0,1]
	v_cvt_pk_fp8_f32 v209, v176, v177 op_sel:[0,0,1]
	v_cvt_pk_fp8_f32 v210, v198, v199 op_sel:[0,0,1]
	v_cvt_pk_fp8_f32 v211, v202, v203 op_sel:[0,0,1]
	s_nop 0
	global_store_dwordx4 v11, v[208:211], s[14:15]
	ds_read_b32 v170, v9
	ds_read_b32 v171, v9 offset:512
	ds_read_b32 v172, v9 offset:1024
	ds_read_b32 v173, v9 offset:1536
	ds_read_b32 v174, v9 offset:2048
	ds_read_b32 v175, v9 offset:2560
	ds_read_b32 v176, v9 offset:3072
	ds_read_b32 v177, v9 offset:3584
	ds_read_b32 v196, v9 offset:4096
	ds_read_b32 v197, v9 offset:4608
	ds_read_b32 v198, v9 offset:5120
	ds_read_b32 v199, v9 offset:5632
	ds_read_b32 v200, v9 offset:6144
	ds_read_b32 v201, v9 offset:6656
	ds_read_b32 v202, v9 offset:7168
	ds_read_b32 v203, v9 offset:7680
	s_waitcnt lgkmcnt(0)
	v_max_f32_e32 v170, v170, v170
	v_max_f32_e32 v171, v171, v171
	v_max_f32_e32 v172, v172, v172
	v_max_f32_e32 v173, v173, v173
	v_max_f32_e32 v174, v174, v174
	v_max_f32_e32 v175, v175, v175
	v_max_f32_e32 v176, v176, v176
	v_max_f32_e32 v177, v177, v177
	v_max_f32_e32 v196, v196, v196
	v_max_f32_e32 v197, v197, v197
	v_max_f32_e32 v198, v198, v198
	v_max_f32_e32 v199, v199, v199
	v_max_f32_e32 v200, v200, v200
	v_max_f32_e32 v201, v201, v201
	v_max_f32_e32 v202, v202, v202
	v_max_f32_e32 v203, v203, v203
	v_med3_f32 v170, v170, s20, v13
	v_med3_f32 v171, v171, s20, v13
	v_med3_f32 v172, v172, s20, v13
	v_med3_f32 v173, v173, s20, v13
	v_med3_f32 v174, v174, s20, v13
	v_med3_f32 v175, v175, s20, v13
	v_med3_f32 v176, v176, s20, v13
	v_med3_f32 v177, v177, s20, v13
	v_med3_f32 v196, v196, s20, v13
	v_med3_f32 v197, v197, s20, v13
	v_med3_f32 v198, v198, s20, v13
	v_med3_f32 v199, v199, s20, v13
	v_med3_f32 v200, v200, s20, v13
	v_med3_f32 v201, v201, s20, v13
	v_med3_f32 v202, v202, s20, v13
	v_med3_f32 v203, v203, s20, v13
	v_mov_b32_e32 v208, 0
	v_mov_b32_e32 v209, 0
	v_mov_b32_e32 v210, 0
	v_mov_b32_e32 v211, 0
	v_cvt_pk_fp8_f32 v208, v170, v171
	v_cvt_pk_fp8_f32 v209, v174, v175
	v_cvt_pk_fp8_f32 v210, v196, v197
	v_cvt_pk_fp8_f32 v211, v200, v201
	v_cvt_pk_fp8_f32 v208, v172, v173 op_sel:[0,0,1]
	v_cvt_pk_fp8_f32 v209, v176, v177 op_sel:[0,0,1]
	v_cvt_pk_fp8_f32 v210, v198, v199 op_sel:[0,0,1]
	v_cvt_pk_fp8_f32 v211, v202, v203 op_sel:[0,0,1]
	s_nop 0
	global_store_dwordx4 v12, v[208:211], s[14:15]
	s_waitcnt vmcnt(32)
	v_mul_f32_e32 v100, 0x43000000, v100
	v_mul_f32_e32 v101, 0x43000000, v101
	v_mul_f32_e32 v102, 0x43000000, v102
	v_mul_f32_e32 v103, 0x43000000, v103
	ds_write_b128 v4, v[100:103]
	v_mul_f32_e32 v104, 0x43000000, v104
	v_mul_f32_e32 v105, 0x43000000, v105
	v_mul_f32_e32 v106, 0x43000000, v106
	v_mul_f32_e32 v107, 0x43000000, v107
	ds_write_b128 v4, v[104:107] offset:1024
	v_mul_f32_e32 v108, 0x43000000, v108
	v_mul_f32_e32 v109, 0x43000000, v109
	v_mul_f32_e32 v110, 0x43000000, v110
	v_mul_f32_e32 v111, 0x43000000, v111
	ds_write_b128 v4, v[108:111] offset:2048
	v_mul_f32_e32 v112, 0x43000000, v112
	v_mul_f32_e32 v113, 0x43000000, v113
	v_mul_f32_e32 v114, 0x43000000, v114
	v_mul_f32_e32 v115, 0x43000000, v115
	ds_write_b128 v4, v[112:115] offset:3072
	v_mul_f32_e32 v116, 0x43000000, v116
	v_mul_f32_e32 v117, 0x43000000, v117
	v_mul_f32_e32 v118, 0x43000000, v118
	v_mul_f32_e32 v119, 0x43000000, v119
	ds_write_b128 v4, v[116:119] offset:4096
	v_mul_f32_e32 v120, 0x43000000, v120
	v_mul_f32_e32 v121, 0x43000000, v121
	v_mul_f32_e32 v122, 0x43000000, v122
	v_mul_f32_e32 v123, 0x43000000, v123
	ds_write_b128 v4, v[120:123] offset:5120
	v_mul_f32_e32 v124, 0x43000000, v124
	v_mul_f32_e32 v125, 0x43000000, v125
	v_mul_f32_e32 v126, 0x43000000, v126
	v_mul_f32_e32 v127, 0x43000000, v127
	ds_write_b128 v4, v[124:127] offset:6144
	v_mul_f32_e32 v128, 0x43000000, v128
	v_mul_f32_e32 v129, 0x43000000, v129
	v_mul_f32_e32 v130, 0x43000000, v130
	v_mul_f32_e32 v131, 0x43000000, v131
	ds_write_b128 v4, v[128:131] offset:7168
	s_waitcnt lgkmcnt(0)
	s_barrier
; #define GAS __attribute__((address_space(1)))
; #define LAS __attribute__((address_space(3)))
; #define LDS_WAIT() asm volatile("s_waitcnt lgkmcnt(0)" ::: "memory")
; __device__ __forceinline__ unsigned pk4_fp8(float a, float b, float c, float d) {
;     a = fminf(fmaxf(a, -448.f), 448.f); b = fminf(fmaxf(b, -448.f), 448.f); c = fminf(fmaxf(c, -448.f), 448.f); d = fminf(fmaxf(d, -448.f), 448.f);
;     int w = __builtin_amdgcn_cvt_pk_fp8_f32(a, b, 0, false); w = __builtin_amdgcn_cvt_pk_fp8_f32(c, d, w, true); return (unsigned)w; }
;     ...
; #pragma unroll
;     for (int i = 0; i < 32; ++i) v[i] = sc >= 0 ? W[(size_t)(k0 + 2 * i + (lane >> 5)) * Nsrc + sc] : 0.f;
; #pragma unroll
;     for (int i = 0; i < 32; ++i) { const int k = k0 + 2 * i + (lane >> 5); float x = v[i] * wscale; if (KS) x *= (k < ksplit ? ksA[k] : ksB[k - ksplit]); scr[(2 * i + (lane >> 5)) * 33 + (lane & 31)] = x; }
;     LDS_WAIT(); asm volatile("" ::: "memory");
;     const int c = lane & 7;
; #pragma unroll
;     for (int j = 0; j < 4; ++j) { const int n = (lane >> 3) + 8 * j; const LAS float* s = scr + (8 * c) * 33 + n;
;         const unsigned long long o = (unsigned long long)pg8::pk4_fp8(s[0 * 33], s[1 * 33], s[2 * 33], s[3 * 33]) | ((unsigned long long)pg8::pk4_fp8(s[4 * 33], s[5 * 33], s[6 * 33], s[7 * 33]) << 32);
;         *(GAS unsigned long long*)(WT + (size_t)(n0 + n) * K + k0 + 8 * c) = o; }
	s_add_i32 s17, s16, 2880
	s_min_u32 s17, s17, 0xfff
	s_lshr_b32 s18, s17, 5
	s_add_i32 s18, s18, 0
	s_and_b32 s19, s17, 31
	s_lshl_b32 s18, s18, 21
	s_lshl_b32 s19, s19, 9
	s_add_u32 s18, s18, s19
	s_add_u32 s12, s2, s18
	s_addc_u32 s13, s3, 0
	global_load_dwordx4 v[100:103], v10, s[12:13]
	s_add_u32 s12, s12, 0x8000
	s_addc_u32 s13, s13, 0
	global_load_dwordx4 v[104:107], v10, s[12:13]
	s_add_u32 s12, s12, 0x8000
	s_addc_u32 s13, s13, 0
	global_load_dwordx4 v[108:111], v10, s[12:13]
	s_add_u32 s12, s12, 0x8000
	s_addc_u32 s13, s13, 0
	global_load_dwordx4 v[112:115], v10, s[12:13]
	s_add_u32 s12, s12, 0x8000
	s_addc_u32 s13, s13, 0
	global_load_dwordx4 v[116:119], v10, s[12:13]
	s_add_u32 s12, s12, 0x8000
	s_addc_u32 s13, s13, 0
	global_load_dwordx4 v[120:123], v10, s[12:13]
	s_add_u32 s12, s12, 0x8000
	s_addc_u32 s13, s13, 0
	global_load_dwordx4 v[124:127], v10, s[12:13]
	s_add_u32 s12, s12, 0x8000
	s_addc_u32 s13, s13, 0
	global_load_dwordx4 v[128:131], v10, s[12:13]
	s_add_i32 s17, s16, 2496
	s_min_u32 s17, s17, 0xfff
	s_lshr_b32 s18, s17, 5
	s_add_i32 s18, s18, 0
	s_and_b32 s19, s17, 31
	s_lshl_b32 s19, s19, 21
	s_lshl_b32 s18, s18, 7
	s_add_u32 s18, s18, s19
	s_add_u32 s14, s4, s18
	s_addc_u32 s15, s5, 0
	ds_read_b32 v170, v6
	ds_read_b32 v171, v6 offset:512
	ds_read_b32 v172, v6 offset:1024
	ds_read_b32 v173, v6 offset:1536
	ds_read_b32 v174, v6 offset:2048
	ds_read_b32 v175, v6 offset:2560
	ds_read_b32 v176, v6 offset:3072
	ds_read_b32 v177, v6 offset:3584
	ds_read_b32 v196, v6 offset:4096
	ds_read_b32 v197, v6 offset:4608
	ds_read_b32 v198, v6 offset:5120
	ds_read_b32 v199, v6 offset:5632
	ds_read_b32 v200, v6 offset:6144
	ds_read_b32 v201, v6 offset:6656
	ds_read_b32 v202, v6 offset:7168
	ds_read_b32 v203, v6 offset:7680
	s_waitcnt lgkmcnt(0)
	v_max_f32_e32 v170, v170, v170
	v_max_f32_e32 v171, v171, v171
	v_max_f32_e32 v172, v172, v172
	v_max_f32_e32 v173, v173, v173
	v_max_f32_e32 v174, v174, v174
	v_max_f32_e32 v175, v175, v175
	v_max_f32_e32 v176, v176, v176
	v_max_f32_e32 v177, v177, v177
	v_max_f32_e32 v196, v196, v196
	v_max_f32_e32 v197, v197, v197
	v_max_f32_e32 v198, v198, v198
	v_max_f32_e32 v199, v199, v199
	v_max_f32_e32 v200, v200, v200
	v_max_f32_e32 v201, v201, v201
	v_max_f32_e32 v202, v202, v202
	v_max_f32_e32 v203, v203, v203
	v_med3_f32 v170, v170, s20, v13
	v_med3_f32 v171, v171, s20, v13
	v_med3_f32 v172, v172, s20, v13
	v_med3_f32 v173, v173, s20, v13
	v_med3_f32 v174, v174, s20, v13
	v_med3_f32 v175, v175, s20, v13
	v_med3_f32 v176, v176, s20, v13
	v_med3_f32 v177, v177, s20, v13
	v_med3_f32 v196, v196, s20, v13
	v_med3_f32 v197, v197, s20, v13
	v_med3_f32 v198, v198, s20, v13
	v_med3_f32 v199, v199, s20, v13
	v_med3_f32 v200, v200, s20, v13
	v_med3_f32 v201, v201, s20, v13
	v_med3_f32 v202, v202, s20, v13
	v_med3_f32 v203, v203, s20, v13
	v_mov_b32_e32 v208, 0
	v_mov_b32_e32 v209, 0
	v_mov_b32_e32 v210, 0
	v_mov_b32_e32 v211, 0
	v_cvt_pk_fp8_f32 v208, v170, v171
	v_cvt_pk_fp8_f32 v209, v174, v175
	v_cvt_pk_fp8_f32 v210, v196, v197
	v_cvt_pk_fp8_f32 v211, v200, v201
	v_cvt_pk_fp8_f32 v208, v172, v173 op_sel:[0,0,1]
	v_cvt_pk_fp8_f32 v209, v176, v177 op_sel:[0,0,1]
	v_cvt_pk_fp8_f32 v210, v198, v199 op_sel:[0,0,1]
	v_cvt_pk_fp8_f32 v211, v202, v203 op_sel:[0,0,1]
	s_nop 0
	global_store_dwordx4 v11, v[208:211], s[14:15]
	ds_read_b32 v170, v8
	ds_read_b32 v171, v8 offset:512
	ds_read_b32 v172, v8 offset:1024
	ds_read_b32 v173, v8 offset:1536
	ds_read_b32 v174, v8 offset:2048
	ds_read_b32 v175, v8 offset:2560
	ds_read_b32 v176, v8 offset:3072
	ds_read_b32 v177, v8 offset:3584
	ds_read_b32 v196, v8 offset:4096
	ds_read_b32 v197, v8 offset:4608
	ds_read_b32 v198, v8 offset:5120
	ds_read_b32 v199, v8 offset:5632
	ds_read_b32 v200, v8 offset:6144
	ds_read_b32 v201, v8 offset:6656
	ds_read_b32 v202, v8 offset:7168
	ds_read_b32 v203, v8 offset:7680
	s_waitcnt lgkmcnt(0)
	v_max_f32_e32 v170, v170, v170
	v_max_f32_e32 v171, v171, v171
	v_max_f32_e32 v172, v172, v172
	v_max_f32_e32 v173, v173, v173
	v_max_f32_e32 v174, v174, v174
	v_max_f32_e32 v175, v175, v175
	v_max_f32_e32 v176, v176, v176
	v_max_f32_e32 v177, v177, v177
	v_max_f32_e32 v196, v196, v196
	v_max_f32_e32 v197, v197, v197
	v_max_f32_e32 v198, v198, v198
	v_max_f32_e32 v199, v199, v199
	v_max_f32_e32 v200, v200, v200
	v_max_f32_e32 v201, v201, v201
	v_max_f32_e32 v202, v202, v202
	v_max_f32_e32 v203, v203, v203
	v_med3_f32 v170, v170, s20, v13
	v_med3_f32 v171, v171, s20, v13
	v_med3_f32 v172, v172, s20, v13
	v_med3_f32 v173, v173, s20, v13
	v_med3_f32 v174, v174, s20, v13
	v_med3_f32 v175, v175, s20, v13
	v_med3_f32 v176, v176, s20, v13
	v_med3_f32 v177, v177, s20, v13
	v_med3_f32 v196, v196, s20, v13
	v_med3_f32 v197, v197, s20, v13
	v_med3_f32 v198, v198, s20, v13
	v_med3_f32 v199, v199, s20, v13
	v_med3_f32 v200, v200, s20, v13
	v_med3_f32 v201, v201, s20, v13
	v_med3_f32 v202, v202, s20, v13
	v_med3_f32 v203, v203, s20, v13
	v_mov_b32_e32 v208, 0
	v_mov_b32_e32 v209, 0
	v_mov_b32_e32 v210, 0
	v_mov_b32_e32 v211, 0
	v_cvt_pk_fp8_f32 v208, v170, v171
	v_cvt_pk_fp8_f32 v209, v174, v175
	v_cvt_pk_fp8_f32 v210, v196, v197
	v_cvt_pk_fp8_f32 v211, v200, v201
	v_cvt_pk_fp8_f32 v208, v172, v173 op_sel:[0,0,1]
	v_cvt_pk_fp8_f32 v209, v176, v177 op_sel:[0,0,1]
	v_cvt_pk_fp8_f32 v210, v198, v199 op_sel:[0,0,1]
	v_cvt_pk_fp8_f32 v211, v202, v203 op_sel:[0,0,1]
	s_nop 0
	global_store_dwordx4 v12, v[208:211], s[14:15]
	s_waitcnt vmcnt(32)
	v_mul_f32_e32 v132, 0x43000000, v132
	v_mul_f32_e32 v133, 0x43000000, v133
	v_mul_f32_e32 v134, 0x43000000, v134
	v_mul_f32_e32 v135, 0x43000000, v135
	ds_write_b128 v5, v[132:135]
	v_mul_f32_e32 v136, 0x43000000, v136
	v_mul_f32_e32 v137, 0x43000000, v137
	v_mul_f32_e32 v138, 0x43000000, v138
	v_mul_f32_e32 v139, 0x43000000, v139
	ds_write_b128 v5, v[136:139] offset:1024
	v_mul_f32_e32 v140, 0x43000000, v140
	v_mul_f32_e32 v141, 0x43000000, v141
	v_mul_f32_e32 v142, 0x43000000, v142
	v_mul_f32_e32 v143, 0x43000000, v143
	ds_write_b128 v5, v[140:143] offset:2048
	v_mul_f32_e32 v144, 0x43000000, v144
	v_mul_f32_e32 v145, 0x43000000, v145
	v_mul_f32_e32 v146, 0x43000000, v146
	v_mul_f32_e32 v147, 0x43000000, v147
	ds_write_b128 v5, v[144:147] offset:3072
	v_mul_f32_e32 v148, 0x43000000, v148
	v_mul_f32_e32 v149, 0x43000000, v149
	v_mul_f32_e32 v150, 0x43000000, v150
	v_mul_f32_e32 v151, 0x43000000, v151
	ds_write_b128 v5, v[148:151] offset:4096
	v_mul_f32_e32 v152, 0x43000000, v152
	v_mul_f32_e32 v153, 0x43000000, v153
	v_mul_f32_e32 v154, 0x43000000, v154
	v_mul_f32_e32 v155, 0x43000000, v155
	ds_write_b128 v5, v[152:155] offset:5120
	v_mul_f32_e32 v156, 0x43000000, v156
	v_mul_f32_e32 v157, 0x43000000, v157
	v_mul_f32_e32 v158, 0x43000000, v158
	v_mul_f32_e32 v159, 0x43000000, v159
	ds_write_b128 v5, v[156:159] offset:6144
	v_mul_f32_e32 v160, 0x43000000, v160
	v_mul_f32_e32 v161, 0x43000000, v161
	v_mul_f32_e32 v162, 0x43000000, v162
	v_mul_f32_e32 v163, 0x43000000, v163
	ds_write_b128 v5, v[160:163] offset:7168
	s_waitcnt lgkmcnt(0)
	s_barrier
; #define GAS __attribute__((address_space(1)))
; #define LAS __attribute__((address_space(3)))
; #define LDS_WAIT() asm volatile("s_waitcnt lgkmcnt(0)" ::: "memory")
; __device__ __forceinline__ unsigned pk4_fp8(float a, float b, float c, float d) {
;     a = fminf(fmaxf(a, -448.f), 448.f); b = fminf(fmaxf(b, -448.f), 448.f); c = fminf(fmaxf(c, -448.f), 448.f); d = fminf(fmaxf(d, -448.f), 448.f);
;     int w = __builtin_amdgcn_cvt_pk_fp8_f32(a, b, 0, false); w = __builtin_amdgcn_cvt_pk_fp8_f32(c, d, w, true); return (unsigned)w; }
;     ...
; #pragma unroll
;     for (int i = 0; i < 32; ++i) v[i] = sc >= 0 ? W[(size_t)(k0 + 2 * i + (lane >> 5)) * Nsrc + sc] : 0.f;
; #pragma unroll
;     for (int i = 0; i < 32; ++i) { const int k = k0 + 2 * i + (lane >> 5); float x = v[i] * wscale; if (KS) x *= (k < ksplit ? ksA[k] : ksB[k - ksplit]); scr[(2 * i + (lane >> 5)) * 33 + (lane & 31)] = x; }
;     LDS_WAIT(); asm volatile("" ::: "memory");
;     const int c = lane & 7;
; #pragma unroll
;     for (int j = 0; j < 4; ++j) { const int n = (lane >> 3) + 8 * j; const LAS float* s = scr + (8 * c) * 33 + n;
;         const unsigned long long o = (unsigned long long)pg8::pk4_fp8(s[0 * 33], s[1 * 33], s[2 * 33], s[3 * 33]) | ((unsigned long long)pg8::pk4_fp8(s[4 * 33], s[5 * 33], s[6 * 33], s[7 * 33]) << 32);
;         *(GAS unsigned long long*)(WT + (size_t)(n0 + n) * K + k0 + 8 * c) = o; }
	s_add_i32 s17, s16, 2976
	s_min_u32 s17, s17, 0xfff
	s_lshr_b32 s18, s17, 5
	s_add_i32 s18, s18, 0
	s_and_b32 s19, s17, 31
	s_lshl_b32 s18, s18, 21
	s_lshl_b32 s19, s19, 9
	s_add_u32 s18, s18, s19
	s_add_u32 s12, s2, s18
	s_addc_u32 s13, s3, 0
	global_load_dwordx4 v[132:135], v10, s[12:13]
	s_add_u32 s12, s12, 0x8000
	s_addc_u32 s13, s13, 0
	global_load_dwordx4 v[136:139], v10, s[12:13]
	s_add_u32 s12, s12, 0x8000
	s_addc_u32 s13, s13, 0
	global_load_dwordx4 v[140:143], v10, s[12:13]
	s_add_u32 s12, s12, 0x8000
	s_addc_u32 s13, s13, 0
	global_load_dwordx4 v[144:147], v10, s[12:13]
	s_add_u32 s12, s12, 0x8000
	s_addc_u32 s13, s13, 0
	global_load_dwordx4 v[148:151], v10, s[12:13]
	s_add_u32 s12, s12, 0x8000
	s_addc_u32 s13, s13, 0
	global_load_dwordx4 v[152:155], v10, s[12:13]
	s_add_u32 s12, s12, 0x8000
	s_addc_u32 s13, s13, 0
	global_load_dwordx4 v[156:159], v10, s[12:13]
	s_add_u32 s12, s12, 0x8000
	s_addc_u32 s13, s13, 0
	global_load_dwordx4 v[160:163], v10, s[12:13]
	s_add_i32 s17, s16, 2592
	s_min_u32 s17, s17, 0xfff
	s_lshr_b32 s18, s17, 5
	s_add_i32 s18, s18, 0
	s_and_b32 s19, s17, 31
	s_lshl_b32 s19, s19, 21
	s_lshl_b32 s18, s18, 7
	s_add_u32 s18, s18, s19
	s_add_u32 s14, s4, s18
	s_addc_u32 s15, s5, 0
	ds_read_b32 v170, v7
	ds_read_b32 v171, v7 offset:512
	ds_read_b32 v172, v7 offset:1024
	ds_read_b32 v173, v7 offset:1536
	ds_read_b32 v174, v7 offset:2048
	ds_read_b32 v175, v7 offset:2560
	ds_read_b32 v176, v7 offset:3072
	ds_read_b32 v177, v7 offset:3584
	ds_read_b32 v196, v7 offset:4096
	ds_read_b32 v197, v7 offset:4608
	ds_read_b32 v198, v7 offset:5120
	ds_read_b32 v199, v7 offset:5632
	ds_read_b32 v200, v7 offset:6144
	ds_read_b32 v201, v7 offset:6656
	ds_read_b32 v202, v7 offset:7168
	ds_read_b32 v203, v7 offset:7680
	s_waitcnt lgkmcnt(0)
	v_max_f32_e32 v170, v170, v170
	v_max_f32_e32 v171, v171, v171
	v_max_f32_e32 v172, v172, v172
	v_max_f32_e32 v173, v173, v173
	v_max_f32_e32 v174, v174, v174
	v_max_f32_e32 v175, v175, v175
	v_max_f32_e32 v176, v176, v176
	v_max_f32_e32 v177, v177, v177
	v_max_f32_e32 v196, v196, v196
	v_max_f32_e32 v197, v197, v197
	v_max_f32_e32 v198, v198, v198
	v_max_f32_e32 v199, v199, v199
	v_max_f32_e32 v200, v200, v200
	v_max_f32_e32 v201, v201, v201
	v_max_f32_e32 v202, v202, v202
	v_max_f32_e32 v203, v203, v203
	v_med3_f32 v170, v170, s20, v13
	v_med3_f32 v171, v171, s20, v13
	v_med3_f32 v172, v172, s20, v13
	v_med3_f32 v173, v173, s20, v13
	v_med3_f32 v174, v174, s20, v13
	v_med3_f32 v175, v175, s20, v13
	v_med3_f32 v176, v176, s20, v13
	v_med3_f32 v177, v177, s20, v13
	v_med3_f32 v196, v196, s20, v13
	v_med3_f32 v197, v197, s20, v13
	v_med3_f32 v198, v198, s20, v13
	v_med3_f32 v199, v199, s20, v13
	v_med3_f32 v200, v200, s20, v13
	v_med3_f32 v201, v201, s20, v13
	v_med3_f32 v202, v202, s20, v13
	v_med3_f32 v203, v203, s20, v13
	v_mov_b32_e32 v208, 0
	v_mov_b32_e32 v209, 0
	v_mov_b32_e32 v210, 0
	v_mov_b32_e32 v211, 0
	v_cvt_pk_fp8_f32 v208, v170, v171
	v_cvt_pk_fp8_f32 v209, v174, v175
	v_cvt_pk_fp8_f32 v210, v196, v197
	v_cvt_pk_fp8_f32 v211, v200, v201
	v_cvt_pk_fp8_f32 v208, v172, v173 op_sel:[0,0,1]
	v_cvt_pk_fp8_f32 v209, v176, v177 op_sel:[0,0,1]
	v_cvt_pk_fp8_f32 v210, v198, v199 op_sel:[0,0,1]
	v_cvt_pk_fp8_f32 v211, v202, v203 op_sel:[0,0,1]
	s_nop 0
	global_store_dwordx4 v11, v[208:211], s[14:15]
	ds_read_b32 v170, v9
	ds_read_b32 v171, v9 offset:512
	ds_read_b32 v172, v9 offset:1024
	ds_read_b32 v173, v9 offset:1536
	ds_read_b32 v174, v9 offset:2048
	ds_read_b32 v175, v9 offset:2560
	ds_read_b32 v176, v9 offset:3072
	ds_read_b32 v177, v9 offset:3584
	ds_read_b32 v196, v9 offset:4096
	ds_read_b32 v197, v9 offset:4608
	ds_read_b32 v198, v9 offset:5120
	ds_read_b32 v199, v9 offset:5632
	ds_read_b32 v200, v9 offset:6144
	ds_read_b32 v201, v9 offset:6656
	ds_read_b32 v202, v9 offset:7168
	ds_read_b32 v203, v9 offset:7680
	s_waitcnt lgkmcnt(0)
	v_max_f32_e32 v170, v170, v170
	v_max_f32_e32 v171, v171, v171
	v_max_f32_e32 v172, v172, v172
	v_max_f32_e32 v173, v173, v173
	v_max_f32_e32 v174, v174, v174
	v_max_f32_e32 v175, v175, v175
	v_max_f32_e32 v176, v176, v176
	v_max_f32_e32 v177, v177, v177
	v_max_f32_e32 v196, v196, v196
	v_max_f32_e32 v197, v197, v197
	v_max_f32_e32 v198, v198, v198
	v_max_f32_e32 v199, v199, v199
	v_max_f32_e32 v200, v200, v200
	v_max_f32_e32 v201, v201, v201
	v_max_f32_e32 v202, v202, v202
	v_max_f32_e32 v203, v203, v203
	v_med3_f32 v170, v170, s20, v13
	v_med3_f32 v171, v171, s20, v13
	v_med3_f32 v172, v172, s20, v13
	v_med3_f32 v173, v173, s20, v13
	v_med3_f32 v174, v174, s20, v13
	v_med3_f32 v175, v175, s20, v13
	v_med3_f32 v176, v176, s20, v13
	v_med3_f32 v177, v177, s20, v13
	v_med3_f32 v196, v196, s20, v13
	v_med3_f32 v197, v197, s20, v13
	v_med3_f32 v198, v198, s20, v13
	v_med3_f32 v199, v199, s20, v13
	v_med3_f32 v200, v200, s20, v13
	v_med3_f32 v201, v201, s20, v13
	v_med3_f32 v202, v202, s20, v13
	v_med3_f32 v203, v203, s20, v13
	v_mov_b32_e32 v208, 0
	v_mov_b32_e32 v209, 0
	v_mov_b32_e32 v210, 0
	v_mov_b32_e32 v211, 0
	v_cvt_pk_fp8_f32 v208, v170, v171
	v_cvt_pk_fp8_f32 v209, v174, v175
	v_cvt_pk_fp8_f32 v210, v196, v197
	v_cvt_pk_fp8_f32 v211, v200, v201
	v_cvt_pk_fp8_f32 v208, v172, v173 op_sel:[0,0,1]
	v_cvt_pk_fp8_f32 v209, v176, v177 op_sel:[0,0,1]
	v_cvt_pk_fp8_f32 v210, v198, v199 op_sel:[0,0,1]
	v_cvt_pk_fp8_f32 v211, v202, v203 op_sel:[0,0,1]
	s_nop 0
	global_store_dwordx4 v12, v[208:211], s[14:15]
	s_waitcnt vmcnt(32)
	v_mul_f32_e32 v36, 0x43000000, v36
	v_mul_f32_e32 v37, 0x43000000, v37
	v_mul_f32_e32 v38, 0x43000000, v38
	v_mul_f32_e32 v39, 0x43000000, v39
	ds_write_b128 v4, v[36:39]
	v_mul_f32_e32 v40, 0x43000000, v40
	v_mul_f32_e32 v41, 0x43000000, v41
	v_mul_f32_e32 v42, 0x43000000, v42
	v_mul_f32_e32 v43, 0x43000000, v43
	ds_write_b128 v4, v[40:43] offset:1024
	v_mul_f32_e32 v44, 0x43000000, v44
	v_mul_f32_e32 v45, 0x43000000, v45
	v_mul_f32_e32 v46, 0x43000000, v46
	v_mul_f32_e32 v47, 0x43000000, v47
	ds_write_b128 v4, v[44:47] offset:2048
	v_mul_f32_e32 v48, 0x43000000, v48
	v_mul_f32_e32 v49, 0x43000000, v49
	v_mul_f32_e32 v50, 0x43000000, v50
	v_mul_f32_e32 v51, 0x43000000, v51
	ds_write_b128 v4, v[48:51] offset:3072
	v_mul_f32_e32 v52, 0x43000000, v52
	v_mul_f32_e32 v53, 0x43000000, v53
	v_mul_f32_e32 v54, 0x43000000, v54
	v_mul_f32_e32 v55, 0x43000000, v55
	ds_write_b128 v4, v[52:55] offset:4096
	v_mul_f32_e32 v56, 0x43000000, v56
	v_mul_f32_e32 v57, 0x43000000, v57
	v_mul_f32_e32 v58, 0x43000000, v58
	v_mul_f32_e32 v59, 0x43000000, v59
	ds_write_b128 v4, v[56:59] offset:5120
	v_mul_f32_e32 v60, 0x43000000, v60
	v_mul_f32_e32 v61, 0x43000000, v61
	v_mul_f32_e32 v62, 0x43000000, v62
	v_mul_f32_e32 v63, 0x43000000, v63
	ds_write_b128 v4, v[60:63] offset:6144
	v_mul_f32_e32 v64, 0x43000000, v64
	v_mul_f32_e32 v65, 0x43000000, v65
	v_mul_f32_e32 v66, 0x43000000, v66
	v_mul_f32_e32 v67, 0x43000000, v67
	ds_write_b128 v4, v[64:67] offset:7168
	s_waitcnt lgkmcnt(0)
	s_barrier
; #define GAS __attribute__((address_space(1)))
; #define LAS __attribute__((address_space(3)))
; #define LDS_WAIT() asm volatile("s_waitcnt lgkmcnt(0)" ::: "memory")
; __device__ __forceinline__ unsigned pk4_fp8(float a, float b, float c, float d) {
;     a = fminf(fmaxf(a, -448.f), 448.f); b = fminf(fmaxf(b, -448.f), 448.f); c = fminf(fmaxf(c, -448.f), 448.f); d = fminf(fmaxf(d, -448.f), 448.f);
;     int w = __builtin_amdgcn_cvt_pk_fp8_f32(a, b, 0, false); w = __builtin_amdgcn_cvt_pk_fp8_f32(c, d, w, true); return (unsigned)w; }
;     ...
; #pragma unroll
;     for (int i = 0; i < 32; ++i) v[i] = sc >= 0 ? W[(size_t)(k0 + 2 * i + (lane >> 5)) * Nsrc + sc] : 0.f;
; #pragma unroll
;     for (int i = 0; i < 32; ++i) { const int k = k0 + 2 * i + (lane >> 5); float x = v[i] * wscale; if (KS) x *= (k < ksplit ? ksA[k] : ksB[k - ksplit]); scr[(2 * i + (lane >> 5)) * 33 + (lane & 31)] = x; }
;     LDS_WAIT(); asm volatile("" ::: "memory");
;     const int c = lane & 7;
; #pragma unroll
;     for (int j = 0; j < 4; ++j) { const int n = (lane >> 3) + 8 * j; const LAS float* s = scr + (8 * c) * 33 + n;
;         const unsigned long long o = (unsigned long long)pg8::pk4_fp8(s[0 * 33], s[1 * 33], s[2 * 33], s[3 * 33]) | ((unsigned long long)pg8::pk4_fp8(s[4 * 33], s[5 * 33], s[6 * 33], s[7 * 33]) << 32);
;         *(GAS unsigned long long*)(WT + (size_t)(n0 + n) * K + k0 + 8 * c) = o; }
	s_add_i32 s17, s16, 3072
	s_min_u32 s17, s17, 0xfff
	s_lshr_b32 s18, s17, 5
	s_add_i32 s18, s18, 0
	s_and_b32 s19, s17, 31
	s_lshl_b32 s18, s18, 21
	s_lshl_b32 s19, s19, 9
	s_add_u32 s18, s18, s19
	s_add_u32 s12, s2, s18
	s_addc_u32 s13, s3, 0
	global_load_dwordx4 v[36:39], v10, s[12:13]
	s_add_u32 s12, s12, 0x8000
	s_addc_u32 s13, s13, 0
	global_load_dwordx4 v[40:43], v10, s[12:13]
	s_add_u32 s12, s12, 0x8000
	s_addc_u32 s13, s13, 0
	global_load_dwordx4 v[44:47], v10, s[12:13]
	s_add_u32 s12, s12, 0x8000
	s_addc_u32 s13, s13, 0
	global_load_dwordx4 v[48:51], v10, s[12:13]
	s_add_u32 s12, s12, 0x8000
	s_addc_u32 s13, s13, 0
	global_load_dwordx4 v[52:55], v10, s[12:13]
	s_add_u32 s12, s12, 0x8000
	s_addc_u32 s13, s13, 0
	global_load_dwordx4 v[56:59], v10, s[12:13]
	s_add_u32 s12, s12, 0x8000
	s_addc_u32 s13, s13, 0
	global_load_dwordx4 v[60:63], v10, s[12:13]
	s_add_u32 s12, s12, 0x8000
	s_addc_u32 s13, s13, 0
	global_load_dwordx4 v[64:67], v10, s[12:13]
	s_add_i32 s17, s16, 2688
	s_min_u32 s17, s17, 0xfff
	s_lshr_b32 s18, s17, 5
	s_add_i32 s18, s18, 0
	s_and_b32 s19, s17, 31
	s_lshl_b32 s19, s19, 21
	s_lshl_b32 s18, s18, 7
	s_add_u32 s18, s18, s19
	s_add_u32 s14, s4, s18
	s_addc_u32 s15, s5, 0
	ds_read_b32 v170, v6
	ds_read_b32 v171, v6 offset:512
	ds_read_b32 v172, v6 offset:1024
	ds_read_b32 v173, v6 offset:1536
	ds_read_b32 v174, v6 offset:2048
	ds_read_b32 v175, v6 offset:2560
	ds_read_b32 v176, v6 offset:3072
	ds_read_b32 v177, v6 offset:3584
	ds_read_b32 v196, v6 offset:4096
	ds_read_b32 v197, v6 offset:4608
	ds_read_b32 v198, v6 offset:5120
	ds_read_b32 v199, v6 offset:5632
	ds_read_b32 v200, v6 offset:6144
	ds_read_b32 v201, v6 offset:6656
	ds_read_b32 v202, v6 offset:7168
	ds_read_b32 v203, v6 offset:7680
	s_waitcnt lgkmcnt(0)
	v_max_f32_e32 v170, v170, v170
	v_max_f32_e32 v171, v171, v171
	v_max_f32_e32 v172, v172, v172
	v_max_f32_e32 v173, v173, v173
	v_max_f32_e32 v174, v174, v174
	v_max_f32_e32 v175, v175, v175
	v_max_f32_e32 v176, v176, v176
	v_max_f32_e32 v177, v177, v177
	v_max_f32_e32 v196, v196, v196
	v_max_f32_e32 v197, v197, v197
	v_max_f32_e32 v198, v198, v198
	v_max_f32_e32 v199, v199, v199
	v_max_f32_e32 v200, v200, v200
	v_max_f32_e32 v201, v201, v201
	v_max_f32_e32 v202, v202, v202
	v_max_f32_e32 v203, v203, v203
	v_med3_f32 v170, v170, s20, v13
	v_med3_f32 v171, v171, s20, v13
	v_med3_f32 v172, v172, s20, v13
	v_med3_f32 v173, v173, s20, v13
	v_med3_f32 v174, v174, s20, v13
	v_med3_f32 v175, v175, s20, v13
	v_med3_f32 v176, v176, s20, v13
	v_med3_f32 v177, v177, s20, v13
	v_med3_f32 v196, v196, s20, v13
	v_med3_f32 v197, v197, s20, v13
	v_med3_f32 v198, v198, s20, v13
	v_med3_f32 v199, v199, s20, v13
	v_med3_f32 v200, v200, s20, v13
	v_med3_f32 v201, v201, s20, v13
	v_med3_f32 v202, v202, s20, v13
	v_med3_f32 v203, v203, s20, v13
	v_mov_b32_e32 v208, 0
	v_mov_b32_e32 v209, 0
	v_mov_b32_e32 v210, 0
	v_mov_b32_e32 v211, 0
	v_cvt_pk_fp8_f32 v208, v170, v171
	v_cvt_pk_fp8_f32 v209, v174, v175
	v_cvt_pk_fp8_f32 v210, v196, v197
	v_cvt_pk_fp8_f32 v211, v200, v201
	v_cvt_pk_fp8_f32 v208, v172, v173 op_sel:[0,0,1]
	v_cvt_pk_fp8_f32 v209, v176, v177 op_sel:[0,0,1]
	v_cvt_pk_fp8_f32 v210, v198, v199 op_sel:[0,0,1]
	v_cvt_pk_fp8_f32 v211, v202, v203 op_sel:[0,0,1]
	s_nop 0
	global_store_dwordx4 v11, v[208:211], s[14:15]
	ds_read_b32 v170, v8
	ds_read_b32 v171, v8 offset:512
	ds_read_b32 v172, v8 offset:1024
	ds_read_b32 v173, v8 offset:1536
	ds_read_b32 v174, v8 offset:2048
	ds_read_b32 v175, v8 offset:2560
	ds_read_b32 v176, v8 offset:3072
	ds_read_b32 v177, v8 offset:3584
	ds_read_b32 v196, v8 offset:4096
	ds_read_b32 v197, v8 offset:4608
	ds_read_b32 v198, v8 offset:5120
	ds_read_b32 v199, v8 offset:5632
	ds_read_b32 v200, v8 offset:6144
	ds_read_b32 v201, v8 offset:6656
	ds_read_b32 v202, v8 offset:7168
	ds_read_b32 v203, v8 offset:7680
	s_waitcnt lgkmcnt(0)
	v_max_f32_e32 v170, v170, v170
	v_max_f32_e32 v171, v171, v171
	v_max_f32_e32 v172, v172, v172
	v_max_f32_e32 v173, v173, v173
	v_max_f32_e32 v174, v174, v174
	v_max_f32_e32 v175, v175, v175
	v_max_f32_e32 v176, v176, v176
	v_max_f32_e32 v177, v177, v177
	v_max_f32_e32 v196, v196, v196
	v_max_f32_e32 v197, v197, v197
	v_max_f32_e32 v198, v198, v198
	v_max_f32_e32 v199, v199, v199
	v_max_f32_e32 v200, v200, v200
	v_max_f32_e32 v201, v201, v201
	v_max_f32_e32 v202, v202, v202
	v_max_f32_e32 v203, v203, v203
	v_med3_f32 v170, v170, s20, v13
	v_med3_f32 v171, v171, s20, v13
	v_med3_f32 v172, v172, s20, v13
	v_med3_f32 v173, v173, s20, v13
	v_med3_f32 v174, v174, s20, v13
	v_med3_f32 v175, v175, s20, v13
	v_med3_f32 v176, v176, s20, v13
	v_med3_f32 v177, v177, s20, v13
	v_med3_f32 v196, v196, s20, v13
	v_med3_f32 v197, v197, s20, v13
	v_med3_f32 v198, v198, s20, v13
	v_med3_f32 v199, v199, s20, v13
	v_med3_f32 v200, v200, s20, v13
	v_med3_f32 v201, v201, s20, v13
	v_med3_f32 v202, v202, s20, v13
	v_med3_f32 v203, v203, s20, v13
	v_mov_b32_e32 v208, 0
	v_mov_b32_e32 v209, 0
	v_mov_b32_e32 v210, 0
	v_mov_b32_e32 v211, 0
	v_cvt_pk_fp8_f32 v208, v170, v171
	v_cvt_pk_fp8_f32 v209, v174, v175
	v_cvt_pk_fp8_f32 v210, v196, v197
	v_cvt_pk_fp8_f32 v211, v200, v201
	v_cvt_pk_fp8_f32 v208, v172, v173 op_sel:[0,0,1]
	v_cvt_pk_fp8_f32 v209, v176, v177 op_sel:[0,0,1]
	v_cvt_pk_fp8_f32 v210, v198, v199 op_sel:[0,0,1]
	v_cvt_pk_fp8_f32 v211, v202, v203 op_sel:[0,0,1]
	s_nop 0
	global_store_dwordx4 v12, v[208:211], s[14:15]
	s_waitcnt vmcnt(32)
	v_mul_f32_e32 v68, 0x43000000, v68
	v_mul_f32_e32 v69, 0x43000000, v69
	v_mul_f32_e32 v70, 0x43000000, v70
	v_mul_f32_e32 v71, 0x43000000, v71
	ds_write_b128 v5, v[68:71]
	v_mul_f32_e32 v72, 0x43000000, v72
	v_mul_f32_e32 v73, 0x43000000, v73
	v_mul_f32_e32 v74, 0x43000000, v74
	v_mul_f32_e32 v75, 0x43000000, v75
	ds_write_b128 v5, v[72:75] offset:1024
	v_mul_f32_e32 v76, 0x43000000, v76
	v_mul_f32_e32 v77, 0x43000000, v77
	v_mul_f32_e32 v78, 0x43000000, v78
	v_mul_f32_e32 v79, 0x43000000, v79
	ds_write_b128 v5, v[76:79] offset:2048
	v_mul_f32_e32 v80, 0x43000000, v80
	v_mul_f32_e32 v81, 0x43000000, v81
	v_mul_f32_e32 v82, 0x43000000, v82
	v_mul_f32_e32 v83, 0x43000000, v83
	ds_write_b128 v5, v[80:83] offset:3072
	v_mul_f32_e32 v84, 0x43000000, v84
	v_mul_f32_e32 v85, 0x43000000, v85
	v_mul_f32_e32 v86, 0x43000000, v86
	v_mul_f32_e32 v87, 0x43000000, v87
	ds_write_b128 v5, v[84:87] offset:4096
	v_mul_f32_e32 v88, 0x43000000, v88
	v_mul_f32_e32 v89, 0x43000000, v89
	v_mul_f32_e32 v90, 0x43000000, v90
	v_mul_f32_e32 v91, 0x43000000, v91
	ds_write_b128 v5, v[88:91] offset:5120
	v_mul_f32_e32 v92, 0x43000000, v92
	v_mul_f32_e32 v93, 0x43000000, v93
	v_mul_f32_e32 v94, 0x43000000, v94
	v_mul_f32_e32 v95, 0x43000000, v95
	ds_write_b128 v5, v[92:95] offset:6144
	v_mul_f32_e32 v96, 0x43000000, v96
	v_mul_f32_e32 v97, 0x43000000, v97
	v_mul_f32_e32 v98, 0x43000000, v98
	v_mul_f32_e32 v99, 0x43000000, v99
	ds_write_b128 v5, v[96:99] offset:7168
	s_waitcnt lgkmcnt(0)
	s_barrier
; #define GAS __attribute__((address_space(1)))
; #define LAS __attribute__((address_space(3)))
; #define LDS_WAIT() asm volatile("s_waitcnt lgkmcnt(0)" ::: "memory")
; __device__ __forceinline__ unsigned pk4_fp8(float a, float b, float c, float d) {
;     a = fminf(fmaxf(a, -448.f), 448.f); b = fminf(fmaxf(b, -448.f), 448.f); c = fminf(fmaxf(c, -448.f), 448.f); d = fminf(fmaxf(d, -448.f), 448.f);
;     int w = __builtin_amdgcn_cvt_pk_fp8_f32(a, b, 0, false); w = __builtin_amdgcn_cvt_pk_fp8_f32(c, d, w, true); return (unsigned)w; }
;     ...
; #pragma unroll
;     for (int i = 0; i < 32; ++i) v[i] = sc >= 0 ? W[(size_t)(k0 + 2 * i + (lane >> 5)) * Nsrc + sc] : 0.f;
; #pragma unroll
;     for (int i = 0; i < 32; ++i) { const int k = k0 + 2 * i + (lane >> 5); float x = v[i] * wscale; if (KS) x *= (k < ksplit ? ksA[k] : ksB[k - ksplit]); scr[(2 * i + (lane >> 5)) * 33 + (lane & 31)] = x; }
;     LDS_WAIT(); asm volatile("" ::: "memory");
;     const int c = lane & 7;
; #pragma unroll
;     for (int j = 0; j < 4; ++j) { const int n = (lane >> 3) + 8 * j; const LAS float* s = scr + (8 * c) * 33 + n;
;         const unsigned long long o = (unsigned long long)pg8::pk4_fp8(s[0 * 33], s[1 * 33], s[2 * 33], s[3 * 33]) | ((unsigned long long)pg8::pk4_fp8(s[4 * 33], s[5 * 33], s[6 * 33], s[7 * 33]) << 32);
;         *(GAS unsigned long long*)(WT + (size_t)(n0 + n) * K + k0 + 8 * c) = o; }
	s_add_i32 s17, s16, 3168
	s_min_u32 s17, s17, 0xfff
	s_lshr_b32 s18, s17, 5
	s_add_i32 s18, s18, 0
	s_and_b32 s19, s17, 31
	s_lshl_b32 s18, s18, 21
	s_lshl_b32 s19, s19, 9
	s_add_u32 s18, s18, s19
	s_add_u32 s12, s2, s18
	s_addc_u32 s13, s3, 0
	global_load_dwordx4 v[68:71], v10, s[12:13]
	s_add_u32 s12, s12, 0x8000
	s_addc_u32 s13, s13, 0
	global_load_dwordx4 v[72:75], v10, s[12:13]
	s_add_u32 s12, s12, 0x8000
	s_addc_u32 s13, s13, 0
	global_load_dwordx4 v[76:79], v10, s[12:13]
	s_add_u32 s12, s12, 0x8000
	s_addc_u32 s13, s13, 0
	global_load_dwordx4 v[80:83], v10, s[12:13]
	s_add_u32 s12, s12, 0x8000
	s_addc_u32 s13, s13, 0
	global_load_dwordx4 v[84:87], v10, s[12:13]
	s_add_u32 s12, s12, 0x8000
	s_addc_u32 s13, s13, 0
	global_load_dwordx4 v[88:91], v10, s[12:13]
	s_add_u32 s12, s12, 0x8000
	s_addc_u32 s13, s13, 0
	global_load_dwordx4 v[92:95], v10, s[12:13]
	s_add_u32 s12, s12, 0x8000
	s_addc_u32 s13, s13, 0
	global_load_dwordx4 v[96:99], v10, s[12:13]
	s_add_i32 s17, s16, 2784
	s_min_u32 s17, s17, 0xfff
	s_lshr_b32 s18, s17, 5
	s_add_i32 s18, s18, 0
	s_and_b32 s19, s17, 31
	s_lshl_b32 s19, s19, 21
	s_lshl_b32 s18, s18, 7
	s_add_u32 s18, s18, s19
	s_add_u32 s14, s4, s18
	s_addc_u32 s15, s5, 0
	ds_read_b32 v170, v7
	ds_read_b32 v171, v7 offset:512
	ds_read_b32 v172, v7 offset:1024
	ds_read_b32 v173, v7 offset:1536
	ds_read_b32 v174, v7 offset:2048
	ds_read_b32 v175, v7 offset:2560
	ds_read_b32 v176, v7 offset:3072
	ds_read_b32 v177, v7 offset:3584
	ds_read_b32 v196, v7 offset:4096
	ds_read_b32 v197, v7 offset:4608
	ds_read_b32 v198, v7 offset:5120
	ds_read_b32 v199, v7 offset:5632
	ds_read_b32 v200, v7 offset:6144
	ds_read_b32 v201, v7 offset:6656
	ds_read_b32 v202, v7 offset:7168
	ds_read_b32 v203, v7 offset:7680
	s_waitcnt lgkmcnt(0)
	v_max_f32_e32 v170, v170, v170
	v_max_f32_e32 v171, v171, v171
	v_max_f32_e32 v172, v172, v172
	v_max_f32_e32 v173, v173, v173
	v_max_f32_e32 v174, v174, v174
	v_max_f32_e32 v175, v175, v175
	v_max_f32_e32 v176, v176, v176
	v_max_f32_e32 v177, v177, v177
	v_max_f32_e32 v196, v196, v196
	v_max_f32_e32 v197, v197, v197
	v_max_f32_e32 v198, v198, v198
	v_max_f32_e32 v199, v199, v199
	v_max_f32_e32 v200, v200, v200
	v_max_f32_e32 v201, v201, v201
	v_max_f32_e32 v202, v202, v202
	v_max_f32_e32 v203, v203, v203
	v_med3_f32 v170, v170, s20, v13
	v_med3_f32 v171, v171, s20, v13
	v_med3_f32 v172, v172, s20, v13
	v_med3_f32 v173, v173, s20, v13
	v_med3_f32 v174, v174, s20, v13
	v_med3_f32 v175, v175, s20, v13
	v_med3_f32 v176, v176, s20, v13
	v_med3_f32 v177, v177, s20, v13
	v_med3_f32 v196, v196, s20, v13
	v_med3_f32 v197, v197, s20, v13
	v_med3_f32 v198, v198, s20, v13
	v_med3_f32 v199, v199, s20, v13
	v_med3_f32 v200, v200, s20, v13
	v_med3_f32 v201, v201, s20, v13
	v_med3_f32 v202, v202, s20, v13
	v_med3_f32 v203, v203, s20, v13
	v_mov_b32_e32 v208, 0
	v_mov_b32_e32 v209, 0
	v_mov_b32_e32 v210, 0
	v_mov_b32_e32 v211, 0
	v_cvt_pk_fp8_f32 v208, v170, v171
	v_cvt_pk_fp8_f32 v209, v174, v175
	v_cvt_pk_fp8_f32 v210, v196, v197
	v_cvt_pk_fp8_f32 v211, v200, v201
	v_cvt_pk_fp8_f32 v208, v172, v173 op_sel:[0,0,1]
	v_cvt_pk_fp8_f32 v209, v176, v177 op_sel:[0,0,1]
	v_cvt_pk_fp8_f32 v210, v198, v199 op_sel:[0,0,1]
	v_cvt_pk_fp8_f32 v211, v202, v203 op_sel:[0,0,1]
	s_nop 0
	global_store_dwordx4 v11, v[208:211], s[14:15]
	ds_read_b32 v170, v9
	ds_read_b32 v171, v9 offset:512
	ds_read_b32 v172, v9 offset:1024
	ds_read_b32 v173, v9 offset:1536
	ds_read_b32 v174, v9 offset:2048
	ds_read_b32 v175, v9 offset:2560
	ds_read_b32 v176, v9 offset:3072
	ds_read_b32 v177, v9 offset:3584
	ds_read_b32 v196, v9 offset:4096
	ds_read_b32 v197, v9 offset:4608
	ds_read_b32 v198, v9 offset:5120
	ds_read_b32 v199, v9 offset:5632
	ds_read_b32 v200, v9 offset:6144
	ds_read_b32 v201, v9 offset:6656
	ds_read_b32 v202, v9 offset:7168
	ds_read_b32 v203, v9 offset:7680
	s_waitcnt lgkmcnt(0)
	v_max_f32_e32 v170, v170, v170
	v_max_f32_e32 v171, v171, v171
	v_max_f32_e32 v172, v172, v172
	v_max_f32_e32 v173, v173, v173
	v_max_f32_e32 v174, v174, v174
	v_max_f32_e32 v175, v175, v175
	v_max_f32_e32 v176, v176, v176
	v_max_f32_e32 v177, v177, v177
	v_max_f32_e32 v196, v196, v196
	v_max_f32_e32 v197, v197, v197
	v_max_f32_e32 v198, v198, v198
	v_max_f32_e32 v199, v199, v199
	v_max_f32_e32 v200, v200, v200
	v_max_f32_e32 v201, v201, v201
	v_max_f32_e32 v202, v202, v202
	v_max_f32_e32 v203, v203, v203
	v_med3_f32 v170, v170, s20, v13
	v_med3_f32 v171, v171, s20, v13
	v_med3_f32 v172, v172, s20, v13
	v_med3_f32 v173, v173, s20, v13
	v_med3_f32 v174, v174, s20, v13
	v_med3_f32 v175, v175, s20, v13
	v_med3_f32 v176, v176, s20, v13
	v_med3_f32 v177, v177, s20, v13
	v_med3_f32 v196, v196, s20, v13
	v_med3_f32 v197, v197, s20, v13
	v_med3_f32 v198, v198, s20, v13
	v_med3_f32 v199, v199, s20, v13
	v_med3_f32 v200, v200, s20, v13
	v_med3_f32 v201, v201, s20, v13
	v_med3_f32 v202, v202, s20, v13
	v_med3_f32 v203, v203, s20, v13
	v_mov_b32_e32 v208, 0
	v_mov_b32_e32 v209, 0
	v_mov_b32_e32 v210, 0
	v_mov_b32_e32 v211, 0
	v_cvt_pk_fp8_f32 v208, v170, v171
	v_cvt_pk_fp8_f32 v209, v174, v175
	v_cvt_pk_fp8_f32 v210, v196, v197
	v_cvt_pk_fp8_f32 v211, v200, v201
	v_cvt_pk_fp8_f32 v208, v172, v173 op_sel:[0,0,1]
	v_cvt_pk_fp8_f32 v209, v176, v177 op_sel:[0,0,1]
	v_cvt_pk_fp8_f32 v210, v198, v199 op_sel:[0,0,1]
	v_cvt_pk_fp8_f32 v211, v202, v203 op_sel:[0,0,1]
	s_nop 0
	global_store_dwordx4 v12, v[208:211], s[14:15]
	s_waitcnt vmcnt(32)
	v_mul_f32_e32 v100, 0x43000000, v100
	v_mul_f32_e32 v101, 0x43000000, v101
	v_mul_f32_e32 v102, 0x43000000, v102
	v_mul_f32_e32 v103, 0x43000000, v103
	ds_write_b128 v4, v[100:103]
	v_mul_f32_e32 v104, 0x43000000, v104
	v_mul_f32_e32 v105, 0x43000000, v105
	v_mul_f32_e32 v106, 0x43000000, v106
	v_mul_f32_e32 v107, 0x43000000, v107
	ds_write_b128 v4, v[104:107] offset:1024
	v_mul_f32_e32 v108, 0x43000000, v108
	v_mul_f32_e32 v109, 0x43000000, v109
	v_mul_f32_e32 v110, 0x43000000, v110
	v_mul_f32_e32 v111, 0x43000000, v111
	ds_write_b128 v4, v[108:111] offset:2048
	v_mul_f32_e32 v112, 0x43000000, v112
	v_mul_f32_e32 v113, 0x43000000, v113
	v_mul_f32_e32 v114, 0x43000000, v114
	v_mul_f32_e32 v115, 0x43000000, v115
	ds_write_b128 v4, v[112:115] offset:3072
	v_mul_f32_e32 v116, 0x43000000, v116
	v_mul_f32_e32 v117, 0x43000000, v117
	v_mul_f32_e32 v118, 0x43000000, v118
	v_mul_f32_e32 v119, 0x43000000, v119
	ds_write_b128 v4, v[116:119] offset:4096
	v_mul_f32_e32 v120, 0x43000000, v120
	v_mul_f32_e32 v121, 0x43000000, v121
	v_mul_f32_e32 v122, 0x43000000, v122
	v_mul_f32_e32 v123, 0x43000000, v123
	ds_write_b128 v4, v[120:123] offset:5120
	v_mul_f32_e32 v124, 0x43000000, v124
	v_mul_f32_e32 v125, 0x43000000, v125
	v_mul_f32_e32 v126, 0x43000000, v126
	v_mul_f32_e32 v127, 0x43000000, v127
	ds_write_b128 v4, v[124:127] offset:6144
	v_mul_f32_e32 v128, 0x43000000, v128
	v_mul_f32_e32 v129, 0x43000000, v129
	v_mul_f32_e32 v130, 0x43000000, v130
	v_mul_f32_e32 v131, 0x43000000, v131
	ds_write_b128 v4, v[128:131] offset:7168
	s_waitcnt lgkmcnt(0)
	s_barrier
; #define GAS __attribute__((address_space(1)))
; #define LAS __attribute__((address_space(3)))
; #define LDS_WAIT() asm volatile("s_waitcnt lgkmcnt(0)" ::: "memory")
; __device__ __forceinline__ unsigned pk4_fp8(float a, float b, float c, float d) {
;     a = fminf(fmaxf(a, -448.f), 448.f); b = fminf(fmaxf(b, -448.f), 448.f); c = fminf(fmaxf(c, -448.f), 448.f); d = fminf(fmaxf(d, -448.f), 448.f);
;     int w = __builtin_amdgcn_cvt_pk_fp8_f32(a, b, 0, false); w = __builtin_amdgcn_cvt_pk_fp8_f32(c, d, w, true); return (unsigned)w; }
;     ...
; #pragma unroll
;     for (int i = 0; i < 32; ++i) v[i] = sc >= 0 ? W[(size_t)(k0 + 2 * i + (lane >> 5)) * Nsrc + sc] : 0.f;
; #pragma unroll
;     for (int i = 0; i < 32; ++i) { const int k = k0 + 2 * i + (lane >> 5); float x = v[i] * wscale; if (KS) x *= (k < ksplit ? ksA[k] : ksB[k - ksplit]); scr[(2 * i + (lane >> 5)) * 33 + (lane & 31)] = x; }
;     LDS_WAIT(); asm volatile("" ::: "memory");
;     const int c = lane & 7;
; #pragma unroll
;     for (int j = 0; j < 4; ++j) { const int n = (lane >> 3) + 8 * j; const LAS float* s = scr + (8 * c) * 33 + n;
;         const unsigned long long o = (unsigned long long)pg8::pk4_fp8(s[0 * 33], s[1 * 33], s[2 * 33], s[3 * 33]) | ((unsigned long long)pg8::pk4_fp8(s[4 * 33], s[5 * 33], s[6 * 33], s[7 * 33]) << 32);
;         *(GAS unsigned long long*)(WT + (size_t)(n0 + n) * K + k0 + 8 * c) = o; }
	s_add_i32 s17, s16, 3264
	s_min_u32 s17, s17, 0xfff
	s_lshr_b32 s18, s17, 5
	s_add_i32 s18, s18, 0
	s_and_b32 s19, s17, 31
	s_lshl_b32 s18, s18, 21
	s_lshl_b32 s19, s19, 9
	s_add_u32 s18, s18, s19
	s_add_u32 s12, s2, s18
	s_addc_u32 s13, s3, 0
	global_load_dwordx4 v[100:103], v10, s[12:13]
	s_add_u32 s12, s12, 0x8000
	s_addc_u32 s13, s13, 0
	global_load_dwordx4 v[104:107], v10, s[12:13]
	s_add_u32 s12, s12, 0x8000
	s_addc_u32 s13, s13, 0
	global_load_dwordx4 v[108:111], v10, s[12:13]
	s_add_u32 s12, s12, 0x8000
	s_addc_u32 s13, s13, 0
	global_load_dwordx4 v[112:115], v10, s[12:13]
	s_add_u32 s12, s12, 0x8000
	s_addc_u32 s13, s13, 0
	global_load_dwordx4 v[116:119], v10, s[12:13]
	s_add_u32 s12, s12, 0x8000
	s_addc_u32 s13, s13, 0
	global_load_dwordx4 v[120:123], v10, s[12:13]
	s_add_u32 s12, s12, 0x8000
	s_addc_u32 s13, s13, 0
	global_load_dwordx4 v[124:127], v10, s[12:13]
	s_add_u32 s12, s12, 0x8000
	s_addc_u32 s13, s13, 0
	global_load_dwordx4 v[128:131], v10, s[12:13]
	s_add_i32 s17, s16, 2880
	s_min_u32 s17, s17, 0xfff
	s_lshr_b32 s18, s17, 5
	s_add_i32 s18, s18, 0
	s_and_b32 s19, s17, 31
	s_lshl_b32 s19, s19, 21
	s_lshl_b32 s18, s18, 7
	s_add_u32 s18, s18, s19
	s_add_u32 s14, s4, s18
	s_addc_u32 s15, s5, 0
	ds_read_b32 v170, v6
	ds_read_b32 v171, v6 offset:512
	ds_read_b32 v172, v6 offset:1024
	ds_read_b32 v173, v6 offset:1536
	ds_read_b32 v174, v6 offset:2048
	ds_read_b32 v175, v6 offset:2560
	ds_read_b32 v176, v6 offset:3072
	ds_read_b32 v177, v6 offset:3584
	ds_read_b32 v196, v6 offset:4096
	ds_read_b32 v197, v6 offset:4608
	ds_read_b32 v198, v6 offset:5120
	ds_read_b32 v199, v6 offset:5632
	ds_read_b32 v200, v6 offset:6144
	ds_read_b32 v201, v6 offset:6656
	ds_read_b32 v202, v6 offset:7168
	ds_read_b32 v203, v6 offset:7680
	s_waitcnt lgkmcnt(0)
	v_max_f32_e32 v170, v170, v170
	v_max_f32_e32 v171, v171, v171
	v_max_f32_e32 v172, v172, v172
	v_max_f32_e32 v173, v173, v173
	v_max_f32_e32 v174, v174, v174
	v_max_f32_e32 v175, v175, v175
	v_max_f32_e32 v176, v176, v176
	v_max_f32_e32 v177, v177, v177
	v_max_f32_e32 v196, v196, v196
	v_max_f32_e32 v197, v197, v197
	v_max_f32_e32 v198, v198, v198
	v_max_f32_e32 v199, v199, v199
	v_max_f32_e32 v200, v200, v200
	v_max_f32_e32 v201, v201, v201
	v_max_f32_e32 v202, v202, v202
	v_max_f32_e32 v203, v203, v203
	v_med3_f32 v170, v170, s20, v13
	v_med3_f32 v171, v171, s20, v13
	v_med3_f32 v172, v172, s20, v13
	v_med3_f32 v173, v173, s20, v13
	v_med3_f32 v174, v174, s20, v13
	v_med3_f32 v175, v175, s20, v13
	v_med3_f32 v176, v176, s20, v13
	v_med3_f32 v177, v177, s20, v13
	v_med3_f32 v196, v196, s20, v13
	v_med3_f32 v197, v197, s20, v13
	v_med3_f32 v198, v198, s20, v13
	v_med3_f32 v199, v199, s20, v13
	v_med3_f32 v200, v200, s20, v13
	v_med3_f32 v201, v201, s20, v13
	v_med3_f32 v202, v202, s20, v13
	v_med3_f32 v203, v203, s20, v13
	v_mov_b32_e32 v208, 0
	v_mov_b32_e32 v209, 0
	v_mov_b32_e32 v210, 0
	v_mov_b32_e32 v211, 0
	v_cvt_pk_fp8_f32 v208, v170, v171
	v_cvt_pk_fp8_f32 v209, v174, v175
	v_cvt_pk_fp8_f32 v210, v196, v197
	v_cvt_pk_fp8_f32 v211, v200, v201
	v_cvt_pk_fp8_f32 v208, v172, v173 op_sel:[0,0,1]
	v_cvt_pk_fp8_f32 v209, v176, v177 op_sel:[0,0,1]
	v_cvt_pk_fp8_f32 v210, v198, v199 op_sel:[0,0,1]
	v_cvt_pk_fp8_f32 v211, v202, v203 op_sel:[0,0,1]
	s_nop 0
	global_store_dwordx4 v11, v[208:211], s[14:15]
	ds_read_b32 v170, v8
	ds_read_b32 v171, v8 offset:512
	ds_read_b32 v172, v8 offset:1024
	ds_read_b32 v173, v8 offset:1536
	ds_read_b32 v174, v8 offset:2048
	ds_read_b32 v175, v8 offset:2560
	ds_read_b32 v176, v8 offset:3072
	ds_read_b32 v177, v8 offset:3584
	ds_read_b32 v196, v8 offset:4096
	ds_read_b32 v197, v8 offset:4608
	ds_read_b32 v198, v8 offset:5120
	ds_read_b32 v199, v8 offset:5632
	ds_read_b32 v200, v8 offset:6144
	ds_read_b32 v201, v8 offset:6656
	ds_read_b32 v202, v8 offset:7168
	ds_read_b32 v203, v8 offset:7680
	s_waitcnt lgkmcnt(0)
	v_max_f32_e32 v170, v170, v170
	v_max_f32_e32 v171, v171, v171
	v_max_f32_e32 v172, v172, v172
	v_max_f32_e32 v173, v173, v173
	v_max_f32_e32 v174, v174, v174
	v_max_f32_e32 v175, v175, v175
	v_max_f32_e32 v176, v176, v176
	v_max_f32_e32 v177, v177, v177
	v_max_f32_e32 v196, v196, v196
	v_max_f32_e32 v197, v197, v197
	v_max_f32_e32 v198, v198, v198
	v_max_f32_e32 v199, v199, v199
	v_max_f32_e32 v200, v200, v200
	v_max_f32_e32 v201, v201, v201
	v_max_f32_e32 v202, v202, v202
	v_max_f32_e32 v203, v203, v203
	v_med3_f32 v170, v170, s20, v13
	v_med3_f32 v171, v171, s20, v13
	v_med3_f32 v172, v172, s20, v13
	v_med3_f32 v173, v173, s20, v13
	v_med3_f32 v174, v174, s20, v13
	v_med3_f32 v175, v175, s20, v13
	v_med3_f32 v176, v176, s20, v13
	v_med3_f32 v177, v177, s20, v13
	v_med3_f32 v196, v196, s20, v13
	v_med3_f32 v197, v197, s20, v13
	v_med3_f32 v198, v198, s20, v13
	v_med3_f32 v199, v199, s20, v13
	v_med3_f32 v200, v200, s20, v13
	v_med3_f32 v201, v201, s20, v13
	v_med3_f32 v202, v202, s20, v13
	v_med3_f32 v203, v203, s20, v13
	v_mov_b32_e32 v208, 0
	v_mov_b32_e32 v209, 0
	v_mov_b32_e32 v210, 0
	v_mov_b32_e32 v211, 0
	v_cvt_pk_fp8_f32 v208, v170, v171
	v_cvt_pk_fp8_f32 v209, v174, v175
	v_cvt_pk_fp8_f32 v210, v196, v197
	v_cvt_pk_fp8_f32 v211, v200, v201
	v_cvt_pk_fp8_f32 v208, v172, v173 op_sel:[0,0,1]
	v_cvt_pk_fp8_f32 v209, v176, v177 op_sel:[0,0,1]
	v_cvt_pk_fp8_f32 v210, v198, v199 op_sel:[0,0,1]
	v_cvt_pk_fp8_f32 v211, v202, v203 op_sel:[0,0,1]
	s_nop 0
	global_store_dwordx4 v12, v[208:211], s[14:15]
	s_waitcnt vmcnt(32)
	v_mul_f32_e32 v132, 0x43000000, v132
	v_mul_f32_e32 v133, 0x43000000, v133
	v_mul_f32_e32 v134, 0x43000000, v134
	v_mul_f32_e32 v135, 0x43000000, v135
	ds_write_b128 v5, v[132:135]
	v_mul_f32_e32 v136, 0x43000000, v136
	v_mul_f32_e32 v137, 0x43000000, v137
	v_mul_f32_e32 v138, 0x43000000, v138
	v_mul_f32_e32 v139, 0x43000000, v139
	ds_write_b128 v5, v[136:139] offset:1024
	v_mul_f32_e32 v140, 0x43000000, v140
	v_mul_f32_e32 v141, 0x43000000, v141
	v_mul_f32_e32 v142, 0x43000000, v142
	v_mul_f32_e32 v143, 0x43000000, v143
	ds_write_b128 v5, v[140:143] offset:2048
	v_mul_f32_e32 v144, 0x43000000, v144
	v_mul_f32_e32 v145, 0x43000000, v145
	v_mul_f32_e32 v146, 0x43000000, v146
	v_mul_f32_e32 v147, 0x43000000, v147
	ds_write_b128 v5, v[144:147] offset:3072
	v_mul_f32_e32 v148, 0x43000000, v148
	v_mul_f32_e32 v149, 0x43000000, v149
	v_mul_f32_e32 v150, 0x43000000, v150
	v_mul_f32_e32 v151, 0x43000000, v151
	ds_write_b128 v5, v[148:151] offset:4096
	v_mul_f32_e32 v152, 0x43000000, v152
	v_mul_f32_e32 v153, 0x43000000, v153
	v_mul_f32_e32 v154, 0x43000000, v154
	v_mul_f32_e32 v155, 0x43000000, v155
	ds_write_b128 v5, v[152:155] offset:5120
	v_mul_f32_e32 v156, 0x43000000, v156
	v_mul_f32_e32 v157, 0x43000000, v157
	v_mul_f32_e32 v158, 0x43000000, v158
	v_mul_f32_e32 v159, 0x43000000, v159
	ds_write_b128 v5, v[156:159] offset:6144
	v_mul_f32_e32 v160, 0x43000000, v160
	v_mul_f32_e32 v161, 0x43000000, v161
	v_mul_f32_e32 v162, 0x43000000, v162
	v_mul_f32_e32 v163, 0x43000000, v163
	ds_write_b128 v5, v[160:163] offset:7168
	s_waitcnt lgkmcnt(0)
	s_barrier
; #define GAS __attribute__((address_space(1)))
; #define LAS __attribute__((address_space(3)))
; #define LDS_WAIT() asm volatile("s_waitcnt lgkmcnt(0)" ::: "memory")
; __device__ __forceinline__ unsigned pk4_fp8(float a, float b, float c, float d) {
;     a = fminf(fmaxf(a, -448.f), 448.f); b = fminf(fmaxf(b, -448.f), 448.f); c = fminf(fmaxf(c, -448.f), 448.f); d = fminf(fmaxf(d, -448.f), 448.f);
;     int w = __builtin_amdgcn_cvt_pk_fp8_f32(a, b, 0, false); w = __builtin_amdgcn_cvt_pk_fp8_f32(c, d, w, true); return (unsigned)w; }
;     ...
; #pragma unroll
;     for (int i = 0; i < 32; ++i) v[i] = sc >= 0 ? W[(size_t)(k0 + 2 * i + (lane >> 5)) * Nsrc + sc] : 0.f;
; #pragma unroll
;     for (int i = 0; i < 32; ++i) { const int k = k0 + 2 * i + (lane >> 5); float x = v[i] * wscale; if (KS) x *= (k < ksplit ? ksA[k] : ksB[k - ksplit]); scr[(2 * i + (lane >> 5)) * 33 + (lane & 31)] = x; }
;     LDS_WAIT(); asm volatile("" ::: "memory");
;     const int c = lane & 7;
; #pragma unroll
;     for (int j = 0; j < 4; ++j) { const int n = (lane >> 3) + 8 * j; const LAS float* s = scr + (8 * c) * 33 + n;
;         const unsigned long long o = (unsigned long long)pg8::pk4_fp8(s[0 * 33], s[1 * 33], s[2 * 33], s[3 * 33]) | ((unsigned long long)pg8::pk4_fp8(s[4 * 33], s[5 * 33], s[6 * 33], s[7 * 33]) << 32);
;         *(GAS unsigned long long*)(WT + (size_t)(n0 + n) * K + k0 + 8 * c) = o; }
	s_add_i32 s17, s16, 3360
	s_min_u32 s17, s17, 0xfff
	s_lshr_b32 s18, s17, 5
	s_add_i32 s18, s18, 0
	s_and_b32 s19, s17, 31
	s_lshl_b32 s18, s18, 21
	s_lshl_b32 s19, s19, 9
	s_add_u32 s18, s18, s19
	s_add_u32 s12, s2, s18
	s_addc_u32 s13, s3, 0
	global_load_dwordx4 v[132:135], v10, s[12:13]
	s_add_u32 s12, s12, 0x8000
	s_addc_u32 s13, s13, 0
	global_load_dwordx4 v[136:139], v10, s[12:13]
	s_add_u32 s12, s12, 0x8000
	s_addc_u32 s13, s13, 0
	global_load_dwordx4 v[140:143], v10, s[12:13]
	s_add_u32 s12, s12, 0x8000
	s_addc_u32 s13, s13, 0
	global_load_dwordx4 v[144:147], v10, s[12:13]
	s_add_u32 s12, s12, 0x8000
	s_addc_u32 s13, s13, 0
	global_load_dwordx4 v[148:151], v10, s[12:13]
	s_add_u32 s12, s12, 0x8000
	s_addc_u32 s13, s13, 0
	global_load_dwordx4 v[152:155], v10, s[12:13]
	s_add_u32 s12, s12, 0x8000
	s_addc_u32 s13, s13, 0
	global_load_dwordx4 v[156:159], v10, s[12:13]
	s_add_u32 s12, s12, 0x8000
	s_addc_u32 s13, s13, 0
	global_load_dwordx4 v[160:163], v10, s[12:13]
	s_add_i32 s17, s16, 2976
	s_min_u32 s17, s17, 0xfff
	s_lshr_b32 s18, s17, 5
	s_add_i32 s18, s18, 0
	s_and_b32 s19, s17, 31
	s_lshl_b32 s19, s19, 21
	s_lshl_b32 s18, s18, 7
	s_add_u32 s18, s18, s19
	s_add_u32 s14, s4, s18
	s_addc_u32 s15, s5, 0
	ds_read_b32 v170, v7
	ds_read_b32 v171, v7 offset:512
	ds_read_b32 v172, v7 offset:1024
	ds_read_b32 v173, v7 offset:1536
	ds_read_b32 v174, v7 offset:2048
	ds_read_b32 v175, v7 offset:2560
	ds_read_b32 v176, v7 offset:3072
	ds_read_b32 v177, v7 offset:3584
	ds_read_b32 v196, v7 offset:4096
	ds_read_b32 v197, v7 offset:4608
	ds_read_b32 v198, v7 offset:5120
	ds_read_b32 v199, v7 offset:5632
	ds_read_b32 v200, v7 offset:6144
	ds_read_b32 v201, v7 offset:6656
	ds_read_b32 v202, v7 offset:7168
	ds_read_b32 v203, v7 offset:7680
	s_waitcnt lgkmcnt(0)
	v_max_f32_e32 v170, v170, v170
	v_max_f32_e32 v171, v171, v171
	v_max_f32_e32 v172, v172, v172
	v_max_f32_e32 v173, v173, v173
	v_max_f32_e32 v174, v174, v174
	v_max_f32_e32 v175, v175, v175
	v_max_f32_e32 v176, v176, v176
	v_max_f32_e32 v177, v177, v177
	v_max_f32_e32 v196, v196, v196
	v_max_f32_e32 v197, v197, v197
	v_max_f32_e32 v198, v198, v198
	v_max_f32_e32 v199, v199, v199
	v_max_f32_e32 v200, v200, v200
	v_max_f32_e32 v201, v201, v201
	v_max_f32_e32 v202, v202, v202
	v_max_f32_e32 v203, v203, v203
	v_med3_f32 v170, v170, s20, v13
	v_med3_f32 v171, v171, s20, v13
	v_med3_f32 v172, v172, s20, v13
	v_med3_f32 v173, v173, s20, v13
	v_med3_f32 v174, v174, s20, v13
	v_med3_f32 v175, v175, s20, v13
	v_med3_f32 v176, v176, s20, v13
	v_med3_f32 v177, v177, s20, v13
	v_med3_f32 v196, v196, s20, v13
	v_med3_f32 v197, v197, s20, v13
	v_med3_f32 v198, v198, s20, v13
	v_med3_f32 v199, v199, s20, v13
	v_med3_f32 v200, v200, s20, v13
	v_med3_f32 v201, v201, s20, v13
	v_med3_f32 v202, v202, s20, v13
	v_med3_f32 v203, v203, s20, v13
	v_mov_b32_e32 v208, 0
	v_mov_b32_e32 v209, 0
	v_mov_b32_e32 v210, 0
	v_mov_b32_e32 v211, 0
	v_cvt_pk_fp8_f32 v208, v170, v171
	v_cvt_pk_fp8_f32 v209, v174, v175
	v_cvt_pk_fp8_f32 v210, v196, v197
	v_cvt_pk_fp8_f32 v211, v200, v201
	v_cvt_pk_fp8_f32 v208, v172, v173 op_sel:[0,0,1]
	v_cvt_pk_fp8_f32 v209, v176, v177 op_sel:[0,0,1]
	v_cvt_pk_fp8_f32 v210, v198, v199 op_sel:[0,0,1]
	v_cvt_pk_fp8_f32 v211, v202, v203 op_sel:[0,0,1]
	s_nop 0
	global_store_dwordx4 v11, v[208:211], s[14:15]
	ds_read_b32 v170, v9
	ds_read_b32 v171, v9 offset:512
	ds_read_b32 v172, v9 offset:1024
	ds_read_b32 v173, v9 offset:1536
	ds_read_b32 v174, v9 offset:2048
	ds_read_b32 v175, v9 offset:2560
	ds_read_b32 v176, v9 offset:3072
	ds_read_b32 v177, v9 offset:3584
	ds_read_b32 v196, v9 offset:4096
	ds_read_b32 v197, v9 offset:4608
	ds_read_b32 v198, v9 offset:5120
	ds_read_b32 v199, v9 offset:5632
	ds_read_b32 v200, v9 offset:6144
	ds_read_b32 v201, v9 offset:6656
	ds_read_b32 v202, v9 offset:7168
	ds_read_b32 v203, v9 offset:7680
	s_waitcnt lgkmcnt(0)
	v_max_f32_e32 v170, v170, v170
	v_max_f32_e32 v171, v171, v171
	v_max_f32_e32 v172, v172, v172
	v_max_f32_e32 v173, v173, v173
	v_max_f32_e32 v174, v174, v174
	v_max_f32_e32 v175, v175, v175
	v_max_f32_e32 v176, v176, v176
	v_max_f32_e32 v177, v177, v177
	v_max_f32_e32 v196, v196, v196
	v_max_f32_e32 v197, v197, v197
	v_max_f32_e32 v198, v198, v198
	v_max_f32_e32 v199, v199, v199
	v_max_f32_e32 v200, v200, v200
	v_max_f32_e32 v201, v201, v201
	v_max_f32_e32 v202, v202, v202
	v_max_f32_e32 v203, v203, v203
	v_med3_f32 v170, v170, s20, v13
	v_med3_f32 v171, v171, s20, v13
	v_med3_f32 v172, v172, s20, v13
	v_med3_f32 v173, v173, s20, v13
	v_med3_f32 v174, v174, s20, v13
	v_med3_f32 v175, v175, s20, v13
	v_med3_f32 v176, v176, s20, v13
	v_med3_f32 v177, v177, s20, v13
	v_med3_f32 v196, v196, s20, v13
	v_med3_f32 v197, v197, s20, v13
	v_med3_f32 v198, v198, s20, v13
	v_med3_f32 v199, v199, s20, v13
	v_med3_f32 v200, v200, s20, v13
	v_med3_f32 v201, v201, s20, v13
	v_med3_f32 v202, v202, s20, v13
	v_med3_f32 v203, v203, s20, v13
	v_mov_b32_e32 v208, 0
	v_mov_b32_e32 v209, 0
	v_mov_b32_e32 v210, 0
	v_mov_b32_e32 v211, 0
	v_cvt_pk_fp8_f32 v208, v170, v171
	v_cvt_pk_fp8_f32 v209, v174, v175
	v_cvt_pk_fp8_f32 v210, v196, v197
	v_cvt_pk_fp8_f32 v211, v200, v201
	v_cvt_pk_fp8_f32 v208, v172, v173 op_sel:[0,0,1]
	v_cvt_pk_fp8_f32 v209, v176, v177 op_sel:[0,0,1]
	v_cvt_pk_fp8_f32 v210, v198, v199 op_sel:[0,0,1]
	v_cvt_pk_fp8_f32 v211, v202, v203 op_sel:[0,0,1]
	s_nop 0
	global_store_dwordx4 v12, v[208:211], s[14:15]
	s_waitcnt vmcnt(32)
	v_mul_f32_e32 v36, 0x43000000, v36
	v_mul_f32_e32 v37, 0x43000000, v37
	v_mul_f32_e32 v38, 0x43000000, v38
	v_mul_f32_e32 v39, 0x43000000, v39
	ds_write_b128 v4, v[36:39]
	v_mul_f32_e32 v40, 0x43000000, v40
	v_mul_f32_e32 v41, 0x43000000, v41
	v_mul_f32_e32 v42, 0x43000000, v42
	v_mul_f32_e32 v43, 0x43000000, v43
	ds_write_b128 v4, v[40:43] offset:1024
	v_mul_f32_e32 v44, 0x43000000, v44
	v_mul_f32_e32 v45, 0x43000000, v45
	v_mul_f32_e32 v46, 0x43000000, v46
	v_mul_f32_e32 v47, 0x43000000, v47
	ds_write_b128 v4, v[44:47] offset:2048
	v_mul_f32_e32 v48, 0x43000000, v48
	v_mul_f32_e32 v49, 0x43000000, v49
	v_mul_f32_e32 v50, 0x43000000, v50
	v_mul_f32_e32 v51, 0x43000000, v51
	ds_write_b128 v4, v[48:51] offset:3072
	v_mul_f32_e32 v52, 0x43000000, v52
	v_mul_f32_e32 v53, 0x43000000, v53
	v_mul_f32_e32 v54, 0x43000000, v54
	v_mul_f32_e32 v55, 0x43000000, v55
	ds_write_b128 v4, v[52:55] offset:4096
	v_mul_f32_e32 v56, 0x43000000, v56
	v_mul_f32_e32 v57, 0x43000000, v57
	v_mul_f32_e32 v58, 0x43000000, v58
	v_mul_f32_e32 v59, 0x43000000, v59
	ds_write_b128 v4, v[56:59] offset:5120
	v_mul_f32_e32 v60, 0x43000000, v60
	v_mul_f32_e32 v61, 0x43000000, v61
	v_mul_f32_e32 v62, 0x43000000, v62
	v_mul_f32_e32 v63, 0x43000000, v63
	ds_write_b128 v4, v[60:63] offset:6144
	v_mul_f32_e32 v64, 0x43000000, v64
	v_mul_f32_e32 v65, 0x43000000, v65
	v_mul_f32_e32 v66, 0x43000000, v66
	v_mul_f32_e32 v67, 0x43000000, v67
	ds_write_b128 v4, v[64:67] offset:7168
	s_waitcnt lgkmcnt(0)
	s_barrier
; #define GAS __attribute__((address_space(1)))
; #define LAS __attribute__((address_space(3)))
; #define LDS_WAIT() asm volatile("s_waitcnt lgkmcnt(0)" ::: "memory")
; __device__ __forceinline__ unsigned pk4_fp8(float a, float b, float c, float d) {
;     a = fminf(fmaxf(a, -448.f), 448.f); b = fminf(fmaxf(b, -448.f), 448.f); c = fminf(fmaxf(c, -448.f), 448.f); d = fminf(fmaxf(d, -448.f), 448.f);
;     int w = __builtin_amdgcn_cvt_pk_fp8_f32(a, b, 0, false); w = __builtin_amdgcn_cvt_pk_fp8_f32(c, d, w, true); return (unsigned)w; }
;     ...
; #pragma unroll
;     for (int i = 0; i < 32; ++i) v[i] = sc >= 0 ? W[(size_t)(k0 + 2 * i + (lane >> 5)) * Nsrc + sc] : 0.f;
; #pragma unroll
;     for (int i = 0; i < 32; ++i) { const int k = k0 + 2 * i + (lane >> 5); float x = v[i] * wscale; if (KS) x *= (k < ksplit ? ksA[k] : ksB[k - ksplit]); scr[(2 * i + (lane >> 5)) * 33 + (lane & 31)] = x; }
;     LDS_WAIT(); asm volatile("" ::: "memory");
;     const int c = lane & 7;
; #pragma unroll
;     for (int j = 0; j < 4; ++j) { const int n = (lane >> 3) + 8 * j; const LAS float* s = scr + (8 * c) * 33 + n;
;         const unsigned long long o = (unsigned long long)pg8::pk4_fp8(s[0 * 33], s[1 * 33], s[2 * 33], s[3 * 33]) | ((unsigned long long)pg8::pk4_fp8(s[4 * 33], s[5 * 33], s[6 * 33], s[7 * 33]) << 32);
;         *(GAS unsigned long long*)(WT + (size_t)(n0 + n) * K + k0 + 8 * c) = o; }
	s_add_i32 s17, s16, 3456
	s_min_u32 s17, s17, 0xfff
	s_lshr_b32 s18, s17, 5
	s_add_i32 s18, s18, 0
	s_and_b32 s19, s17, 31
	s_lshl_b32 s18, s18, 21
	s_lshl_b32 s19, s19, 9
	s_add_u32 s18, s18, s19
	s_add_u32 s12, s2, s18
	s_addc_u32 s13, s3, 0
	global_load_dwordx4 v[36:39], v10, s[12:13]
	s_add_u32 s12, s12, 0x8000
	s_addc_u32 s13, s13, 0
	global_load_dwordx4 v[40:43], v10, s[12:13]
	s_add_u32 s12, s12, 0x8000
	s_addc_u32 s13, s13, 0
	global_load_dwordx4 v[44:47], v10, s[12:13]
	s_add_u32 s12, s12, 0x8000
	s_addc_u32 s13, s13, 0
	global_load_dwordx4 v[48:51], v10, s[12:13]
	s_add_u32 s12, s12, 0x8000
	s_addc_u32 s13, s13, 0
	global_load_dwordx4 v[52:55], v10, s[12:13]
	s_add_u32 s12, s12, 0x8000
	s_addc_u32 s13, s13, 0
	global_load_dwordx4 v[56:59], v10, s[12:13]
	s_add_u32 s12, s12, 0x8000
	s_addc_u32 s13, s13, 0
	global_load_dwordx4 v[60:63], v10, s[12:13]
	s_add_u32 s12, s12, 0x8000
	s_addc_u32 s13, s13, 0
	global_load_dwordx4 v[64:67], v10, s[12:13]
	s_add_i32 s17, s16, 3072
	s_min_u32 s17, s17, 0xfff
	s_lshr_b32 s18, s17, 5
	s_add_i32 s18, s18, 0
	s_and_b32 s19, s17, 31
	s_lshl_b32 s19, s19, 21
	s_lshl_b32 s18, s18, 7
	s_add_u32 s18, s18, s19
	s_add_u32 s14, s4, s18
	s_addc_u32 s15, s5, 0
	ds_read_b32 v170, v6
	ds_read_b32 v171, v6 offset:512
	ds_read_b32 v172, v6 offset:1024
	ds_read_b32 v173, v6 offset:1536
	ds_read_b32 v174, v6 offset:2048
	ds_read_b32 v175, v6 offset:2560
	ds_read_b32 v176, v6 offset:3072
	ds_read_b32 v177, v6 offset:3584
	ds_read_b32 v196, v6 offset:4096
	ds_read_b32 v197, v6 offset:4608
	ds_read_b32 v198, v6 offset:5120
	ds_read_b32 v199, v6 offset:5632
	ds_read_b32 v200, v6 offset:6144
	ds_read_b32 v201, v6 offset:6656
	ds_read_b32 v202, v6 offset:7168
	ds_read_b32 v203, v6 offset:7680
	s_waitcnt lgkmcnt(0)
	v_max_f32_e32 v170, v170, v170
	v_max_f32_e32 v171, v171, v171
	v_max_f32_e32 v172, v172, v172
	v_max_f32_e32 v173, v173, v173
	v_max_f32_e32 v174, v174, v174
	v_max_f32_e32 v175, v175, v175
	v_max_f32_e32 v176, v176, v176
	v_max_f32_e32 v177, v177, v177
	v_max_f32_e32 v196, v196, v196
	v_max_f32_e32 v197, v197, v197
	v_max_f32_e32 v198, v198, v198
	v_max_f32_e32 v199, v199, v199
	v_max_f32_e32 v200, v200, v200
	v_max_f32_e32 v201, v201, v201
	v_max_f32_e32 v202, v202, v202
	v_max_f32_e32 v203, v203, v203
	v_med3_f32 v170, v170, s20, v13
	v_med3_f32 v171, v171, s20, v13
	v_med3_f32 v172, v172, s20, v13
	v_med3_f32 v173, v173, s20, v13
	v_med3_f32 v174, v174, s20, v13
	v_med3_f32 v175, v175, s20, v13
	v_med3_f32 v176, v176, s20, v13
	v_med3_f32 v177, v177, s20, v13
	v_med3_f32 v196, v196, s20, v13
	v_med3_f32 v197, v197, s20, v13
	v_med3_f32 v198, v198, s20, v13
	v_med3_f32 v199, v199, s20, v13
	v_med3_f32 v200, v200, s20, v13
	v_med3_f32 v201, v201, s20, v13
	v_med3_f32 v202, v202, s20, v13
	v_med3_f32 v203, v203, s20, v13
	v_mov_b32_e32 v208, 0
	v_mov_b32_e32 v209, 0
	v_mov_b32_e32 v210, 0
	v_mov_b32_e32 v211, 0
	v_cvt_pk_fp8_f32 v208, v170, v171
	v_cvt_pk_fp8_f32 v209, v174, v175
	v_cvt_pk_fp8_f32 v210, v196, v197
	v_cvt_pk_fp8_f32 v211, v200, v201
	v_cvt_pk_fp8_f32 v208, v172, v173 op_sel:[0,0,1]
	v_cvt_pk_fp8_f32 v209, v176, v177 op_sel:[0,0,1]
	v_cvt_pk_fp8_f32 v210, v198, v199 op_sel:[0,0,1]
	v_cvt_pk_fp8_f32 v211, v202, v203 op_sel:[0,0,1]
	s_nop 0
	global_store_dwordx4 v11, v[208:211], s[14:15]
	ds_read_b32 v170, v8
	ds_read_b32 v171, v8 offset:512
	ds_read_b32 v172, v8 offset:1024
	ds_read_b32 v173, v8 offset:1536
	ds_read_b32 v174, v8 offset:2048
	ds_read_b32 v175, v8 offset:2560
	ds_read_b32 v176, v8 offset:3072
	ds_read_b32 v177, v8 offset:3584
	ds_read_b32 v196, v8 offset:4096
	ds_read_b32 v197, v8 offset:4608
	ds_read_b32 v198, v8 offset:5120
	ds_read_b32 v199, v8 offset:5632
	ds_read_b32 v200, v8 offset:6144
	ds_read_b32 v201, v8 offset:6656
	ds_read_b32 v202, v8 offset:7168
	ds_read_b32 v203, v8 offset:7680
	s_waitcnt lgkmcnt(0)
	v_max_f32_e32 v170, v170, v170
	v_max_f32_e32 v171, v171, v171
	v_max_f32_e32 v172, v172, v172
	v_max_f32_e32 v173, v173, v173
	v_max_f32_e32 v174, v174, v174
	v_max_f32_e32 v175, v175, v175
	v_max_f32_e32 v176, v176, v176
	v_max_f32_e32 v177, v177, v177
	v_max_f32_e32 v196, v196, v196
	v_max_f32_e32 v197, v197, v197
	v_max_f32_e32 v198, v198, v198
	v_max_f32_e32 v199, v199, v199
	v_max_f32_e32 v200, v200, v200
	v_max_f32_e32 v201, v201, v201
	v_max_f32_e32 v202, v202, v202
	v_max_f32_e32 v203, v203, v203
	v_med3_f32 v170, v170, s20, v13
	v_med3_f32 v171, v171, s20, v13
	v_med3_f32 v172, v172, s20, v13
	v_med3_f32 v173, v173, s20, v13
	v_med3_f32 v174, v174, s20, v13
	v_med3_f32 v175, v175, s20, v13
	v_med3_f32 v176, v176, s20, v13
	v_med3_f32 v177, v177, s20, v13
	v_med3_f32 v196, v196, s20, v13
	v_med3_f32 v197, v197, s20, v13
	v_med3_f32 v198, v198, s20, v13
	v_med3_f32 v199, v199, s20, v13
	v_med3_f32 v200, v200, s20, v13
	v_med3_f32 v201, v201, s20, v13
	v_med3_f32 v202, v202, s20, v13
	v_med3_f32 v203, v203, s20, v13
	v_mov_b32_e32 v208, 0
	v_mov_b32_e32 v209, 0
	v_mov_b32_e32 v210, 0
	v_mov_b32_e32 v211, 0
	v_cvt_pk_fp8_f32 v208, v170, v171
	v_cvt_pk_fp8_f32 v209, v174, v175
	v_cvt_pk_fp8_f32 v210, v196, v197
	v_cvt_pk_fp8_f32 v211, v200, v201
	v_cvt_pk_fp8_f32 v208, v172, v173 op_sel:[0,0,1]
	v_cvt_pk_fp8_f32 v209, v176, v177 op_sel:[0,0,1]
	v_cvt_pk_fp8_f32 v210, v198, v199 op_sel:[0,0,1]
	v_cvt_pk_fp8_f32 v211, v202, v203 op_sel:[0,0,1]
	s_nop 0
	global_store_dwordx4 v12, v[208:211], s[14:15]
	s_waitcnt vmcnt(32)
	v_mul_f32_e32 v68, 0x43000000, v68
	v_mul_f32_e32 v69, 0x43000000, v69
	v_mul_f32_e32 v70, 0x43000000, v70
	v_mul_f32_e32 v71, 0x43000000, v71
	ds_write_b128 v5, v[68:71]
	v_mul_f32_e32 v72, 0x43000000, v72
	v_mul_f32_e32 v73, 0x43000000, v73
	v_mul_f32_e32 v74, 0x43000000, v74
	v_mul_f32_e32 v75, 0x43000000, v75
	ds_write_b128 v5, v[72:75] offset:1024
	v_mul_f32_e32 v76, 0x43000000, v76
	v_mul_f32_e32 v77, 0x43000000, v77
	v_mul_f32_e32 v78, 0x43000000, v78
	v_mul_f32_e32 v79, 0x43000000, v79
	ds_write_b128 v5, v[76:79] offset:2048
	v_mul_f32_e32 v80, 0x43000000, v80
	v_mul_f32_e32 v81, 0x43000000, v81
	v_mul_f32_e32 v82, 0x43000000, v82
	v_mul_f32_e32 v83, 0x43000000, v83
	ds_write_b128 v5, v[80:83] offset:3072
	v_mul_f32_e32 v84, 0x43000000, v84
	v_mul_f32_e32 v85, 0x43000000, v85
	v_mul_f32_e32 v86, 0x43000000, v86
	v_mul_f32_e32 v87, 0x43000000, v87
	ds_write_b128 v5, v[84:87] offset:4096
	v_mul_f32_e32 v88, 0x43000000, v88
	v_mul_f32_e32 v89, 0x43000000, v89
	v_mul_f32_e32 v90, 0x43000000, v90
	v_mul_f32_e32 v91, 0x43000000, v91
	ds_write_b128 v5, v[88:91] offset:5120
	v_mul_f32_e32 v92, 0x43000000, v92
	v_mul_f32_e32 v93, 0x43000000, v93
	v_mul_f32_e32 v94, 0x43000000, v94
	v_mul_f32_e32 v95, 0x43000000, v95
	ds_write_b128 v5, v[92:95] offset:6144
	v_mul_f32_e32 v96, 0x43000000, v96
	v_mul_f32_e32 v97, 0x43000000, v97
	v_mul_f32_e32 v98, 0x43000000, v98
	v_mul_f32_e32 v99, 0x43000000, v99
	ds_write_b128 v5, v[96:99] offset:7168
	s_waitcnt lgkmcnt(0)
	s_barrier
; #define GAS __attribute__((address_space(1)))
; #define LAS __attribute__((address_space(3)))
; #define LDS_WAIT() asm volatile("s_waitcnt lgkmcnt(0)" ::: "memory")
; __device__ __forceinline__ unsigned pk4_fp8(float a, float b, float c, float d) {
;     a = fminf(fmaxf(a, -448.f), 448.f); b = fminf(fmaxf(b, -448.f), 448.f); c = fminf(fmaxf(c, -448.f), 448.f); d = fminf(fmaxf(d, -448.f), 448.f);
;     int w = __builtin_amdgcn_cvt_pk_fp8_f32(a, b, 0, false); w = __builtin_amdgcn_cvt_pk_fp8_f32(c, d, w, true); return (unsigned)w; }
;     ...
; #pragma unroll
;     for (int i = 0; i < 32; ++i) v[i] = sc >= 0 ? W[(size_t)(k0 + 2 * i + (lane >> 5)) * Nsrc + sc] : 0.f;
; #pragma unroll
;     for (int i = 0; i < 32; ++i) { const int k = k0 + 2 * i + (lane >> 5); float x = v[i] * wscale; if (KS) x *= (k < ksplit ? ksA[k] : ksB[k - ksplit]); scr[(2 * i + (lane >> 5)) * 33 + (lane & 31)] = x; }
;     LDS_WAIT(); asm volatile("" ::: "memory");
;     const int c = lane & 7;
; #pragma unroll
;     for (int j = 0; j < 4; ++j) { const int n = (lane >> 3) + 8 * j; const LAS float* s = scr + (8 * c) * 33 + n;
;         const unsigned long long o = (unsigned long long)pg8::pk4_fp8(s[0 * 33], s[1 * 33], s[2 * 33], s[3 * 33]) | ((unsigned long long)pg8::pk4_fp8(s[4 * 33], s[5 * 33], s[6 * 33], s[7 * 33]) << 32);
;         *(GAS unsigned long long*)(WT + (size_t)(n0 + n) * K + k0 + 8 * c) = o; }
	s_add_i32 s17, s16, 3552
	s_min_u32 s17, s17, 0xfff
	s_lshr_b32 s18, s17, 5
	s_add_i32 s18, s18, 0
	s_and_b32 s19, s17, 31
	s_lshl_b32 s18, s18, 21
	s_lshl_b32 s19, s19, 9
	s_add_u32 s18, s18, s19
	s_add_u32 s12, s2, s18
	s_addc_u32 s13, s3, 0
	global_load_dwordx4 v[68:71], v10, s[12:13]
	s_add_u32 s12, s12, 0x8000
	s_addc_u32 s13, s13, 0
	global_load_dwordx4 v[72:75], v10, s[12:13]
	s_add_u32 s12, s12, 0x8000
	s_addc_u32 s13, s13, 0
	global_load_dwordx4 v[76:79], v10, s[12:13]
	s_add_u32 s12, s12, 0x8000
	s_addc_u32 s13, s13, 0
	global_load_dwordx4 v[80:83], v10, s[12:13]
	s_add_u32 s12, s12, 0x8000
	s_addc_u32 s13, s13, 0
	global_load_dwordx4 v[84:87], v10, s[12:13]
	s_add_u32 s12, s12, 0x8000
	s_addc_u32 s13, s13, 0
	global_load_dwordx4 v[88:91], v10, s[12:13]
	s_add_u32 s12, s12, 0x8000
	s_addc_u32 s13, s13, 0
	global_load_dwordx4 v[92:95], v10, s[12:13]
	s_add_u32 s12, s12, 0x8000
	s_addc_u32 s13, s13, 0
	global_load_dwordx4 v[96:99], v10, s[12:13]
	s_add_i32 s17, s16, 3168
	s_min_u32 s17, s17, 0xfff
	s_lshr_b32 s18, s17, 5
	s_add_i32 s18, s18, 0
	s_and_b32 s19, s17, 31
	s_lshl_b32 s19, s19, 21
	s_lshl_b32 s18, s18, 7
	s_add_u32 s18, s18, s19
	s_add_u32 s14, s4, s18
	s_addc_u32 s15, s5, 0
	ds_read_b32 v170, v7
	ds_read_b32 v171, v7 offset:512
	ds_read_b32 v172, v7 offset:1024
	ds_read_b32 v173, v7 offset:1536
	ds_read_b32 v174, v7 offset:2048
	ds_read_b32 v175, v7 offset:2560
	ds_read_b32 v176, v7 offset:3072
	ds_read_b32 v177, v7 offset:3584
	ds_read_b32 v196, v7 offset:4096
	ds_read_b32 v197, v7 offset:4608
	ds_read_b32 v198, v7 offset:5120
	ds_read_b32 v199, v7 offset:5632
	ds_read_b32 v200, v7 offset:6144
	ds_read_b32 v201, v7 offset:6656
	ds_read_b32 v202, v7 offset:7168
	ds_read_b32 v203, v7 offset:7680
	s_waitcnt lgkmcnt(0)
	v_max_f32_e32 v170, v170, v170
	v_max_f32_e32 v171, v171, v171
	v_max_f32_e32 v172, v172, v172
	v_max_f32_e32 v173, v173, v173
	v_max_f32_e32 v174, v174, v174
	v_max_f32_e32 v175, v175, v175
	v_max_f32_e32 v176, v176, v176
	v_max_f32_e32 v177, v177, v177
	v_max_f32_e32 v196, v196, v196
	v_max_f32_e32 v197, v197, v197
	v_max_f32_e32 v198, v198, v198
	v_max_f32_e32 v199, v199, v199
	v_max_f32_e32 v200, v200, v200
	v_max_f32_e32 v201, v201, v201
	v_max_f32_e32 v202, v202, v202
	v_max_f32_e32 v203, v203, v203
	v_med3_f32 v170, v170, s20, v13
	v_med3_f32 v171, v171, s20, v13
	v_med3_f32 v172, v172, s20, v13
	v_med3_f32 v173, v173, s20, v13
	v_med3_f32 v174, v174, s20, v13
	v_med3_f32 v175, v175, s20, v13
	v_med3_f32 v176, v176, s20, v13
	v_med3_f32 v177, v177, s20, v13
	v_med3_f32 v196, v196, s20, v13
	v_med3_f32 v197, v197, s20, v13
	v_med3_f32 v198, v198, s20, v13
	v_med3_f32 v199, v199, s20, v13
	v_med3_f32 v200, v200, s20, v13
	v_med3_f32 v201, v201, s20, v13
	v_med3_f32 v202, v202, s20, v13
	v_med3_f32 v203, v203, s20, v13
	v_mov_b32_e32 v208, 0
	v_mov_b32_e32 v209, 0
	v_mov_b32_e32 v210, 0
	v_mov_b32_e32 v211, 0
	v_cvt_pk_fp8_f32 v208, v170, v171
	v_cvt_pk_fp8_f32 v209, v174, v175
	v_cvt_pk_fp8_f32 v210, v196, v197
	v_cvt_pk_fp8_f32 v211, v200, v201
	v_cvt_pk_fp8_f32 v208, v172, v173 op_sel:[0,0,1]
	v_cvt_pk_fp8_f32 v209, v176, v177 op_sel:[0,0,1]
	v_cvt_pk_fp8_f32 v210, v198, v199 op_sel:[0,0,1]
	v_cvt_pk_fp8_f32 v211, v202, v203 op_sel:[0,0,1]
	s_nop 0
	global_store_dwordx4 v11, v[208:211], s[14:15]
	ds_read_b32 v170, v9
	ds_read_b32 v171, v9 offset:512
	ds_read_b32 v172, v9 offset:1024
	ds_read_b32 v173, v9 offset:1536
	ds_read_b32 v174, v9 offset:2048
	ds_read_b32 v175, v9 offset:2560
	ds_read_b32 v176, v9 offset:3072
	ds_read_b32 v177, v9 offset:3584
	ds_read_b32 v196, v9 offset:4096
	ds_read_b32 v197, v9 offset:4608
	ds_read_b32 v198, v9 offset:5120
	ds_read_b32 v199, v9 offset:5632
	ds_read_b32 v200, v9 offset:6144
	ds_read_b32 v201, v9 offset:6656
	ds_read_b32 v202, v9 offset:7168
	ds_read_b32 v203, v9 offset:7680
	s_waitcnt lgkmcnt(0)
	v_max_f32_e32 v170, v170, v170
	v_max_f32_e32 v171, v171, v171
	v_max_f32_e32 v172, v172, v172
	v_max_f32_e32 v173, v173, v173
	v_max_f32_e32 v174, v174, v174
	v_max_f32_e32 v175, v175, v175
	v_max_f32_e32 v176, v176, v176
	v_max_f32_e32 v177, v177, v177
	v_max_f32_e32 v196, v196, v196
	v_max_f32_e32 v197, v197, v197
	v_max_f32_e32 v198, v198, v198
	v_max_f32_e32 v199, v199, v199
	v_max_f32_e32 v200, v200, v200
	v_max_f32_e32 v201, v201, v201
	v_max_f32_e32 v202, v202, v202
	v_max_f32_e32 v203, v203, v203
	v_med3_f32 v170, v170, s20, v13
	v_med3_f32 v171, v171, s20, v13
	v_med3_f32 v172, v172, s20, v13
	v_med3_f32 v173, v173, s20, v13
	v_med3_f32 v174, v174, s20, v13
	v_med3_f32 v175, v175, s20, v13
	v_med3_f32 v176, v176, s20, v13
	v_med3_f32 v177, v177, s20, v13
	v_med3_f32 v196, v196, s20, v13
	v_med3_f32 v197, v197, s20, v13
	v_med3_f32 v198, v198, s20, v13
	v_med3_f32 v199, v199, s20, v13
	v_med3_f32 v200, v200, s20, v13
	v_med3_f32 v201, v201, s20, v13
	v_med3_f32 v202, v202, s20, v13
	v_med3_f32 v203, v203, s20, v13
	v_mov_b32_e32 v208, 0
	v_mov_b32_e32 v209, 0
	v_mov_b32_e32 v210, 0
	v_mov_b32_e32 v211, 0
	v_cvt_pk_fp8_f32 v208, v170, v171
	v_cvt_pk_fp8_f32 v209, v174, v175
	v_cvt_pk_fp8_f32 v210, v196, v197
	v_cvt_pk_fp8_f32 v211, v200, v201
	v_cvt_pk_fp8_f32 v208, v172, v173 op_sel:[0,0,1]
	v_cvt_pk_fp8_f32 v209, v176, v177 op_sel:[0,0,1]
	v_cvt_pk_fp8_f32 v210, v198, v199 op_sel:[0,0,1]
	v_cvt_pk_fp8_f32 v211, v202, v203 op_sel:[0,0,1]
	s_nop 0
	global_store_dwordx4 v12, v[208:211], s[14:15]
	s_waitcnt vmcnt(32)
	v_mul_f32_e32 v100, 0x43000000, v100
	v_mul_f32_e32 v101, 0x43000000, v101
	v_mul_f32_e32 v102, 0x43000000, v102
	v_mul_f32_e32 v103, 0x43000000, v103
	ds_write_b128 v4, v[100:103]
	v_mul_f32_e32 v104, 0x43000000, v104
	v_mul_f32_e32 v105, 0x43000000, v105
	v_mul_f32_e32 v106, 0x43000000, v106
	v_mul_f32_e32 v107, 0x43000000, v107
	ds_write_b128 v4, v[104:107] offset:1024
	v_mul_f32_e32 v108, 0x43000000, v108
	v_mul_f32_e32 v109, 0x43000000, v109
	v_mul_f32_e32 v110, 0x43000000, v110
	v_mul_f32_e32 v111, 0x43000000, v111
	ds_write_b128 v4, v[108:111] offset:2048
	v_mul_f32_e32 v112, 0x43000000, v112
	v_mul_f32_e32 v113, 0x43000000, v113
	v_mul_f32_e32 v114, 0x43000000, v114
	v_mul_f32_e32 v115, 0x43000000, v115
	ds_write_b128 v4, v[112:115] offset:3072
	v_mul_f32_e32 v116, 0x43000000, v116
	v_mul_f32_e32 v117, 0x43000000, v117
	v_mul_f32_e32 v118, 0x43000000, v118
	v_mul_f32_e32 v119, 0x43000000, v119
	ds_write_b128 v4, v[116:119] offset:4096
	v_mul_f32_e32 v120, 0x43000000, v120
	v_mul_f32_e32 v121, 0x43000000, v121
	v_mul_f32_e32 v122, 0x43000000, v122
	v_mul_f32_e32 v123, 0x43000000, v123
	ds_write_b128 v4, v[120:123] offset:5120
	v_mul_f32_e32 v124, 0x43000000, v124
	v_mul_f32_e32 v125, 0x43000000, v125
	v_mul_f32_e32 v126, 0x43000000, v126
	v_mul_f32_e32 v127, 0x43000000, v127
	ds_write_b128 v4, v[124:127] offset:6144
	v_mul_f32_e32 v128, 0x43000000, v128
	v_mul_f32_e32 v129, 0x43000000, v129
	v_mul_f32_e32 v130, 0x43000000, v130
	v_mul_f32_e32 v131, 0x43000000, v131
	ds_write_b128 v4, v[128:131] offset:7168
	s_waitcnt lgkmcnt(0)
	s_barrier
; #define GAS __attribute__((address_space(1)))
; #define LAS __attribute__((address_space(3)))
; #define LDS_WAIT() asm volatile("s_waitcnt lgkmcnt(0)" ::: "memory")
; __device__ __forceinline__ unsigned pk4_fp8(float a, float b, float c, float d) {
;     a = fminf(fmaxf(a, -448.f), 448.f); b = fminf(fmaxf(b, -448.f), 448.f); c = fminf(fmaxf(c, -448.f), 448.f); d = fminf(fmaxf(d, -448.f), 448.f);
;     int w = __builtin_amdgcn_cvt_pk_fp8_f32(a, b, 0, false); w = __builtin_amdgcn_cvt_pk_fp8_f32(c, d, w, true); return (unsigned)w; }
;     ...
; #pragma unroll
;     for (int i = 0; i < 32; ++i) v[i] = sc >= 0 ? W[(size_t)(k0 + 2 * i + (lane >> 5)) * Nsrc + sc] : 0.f;
; #pragma unroll
;     for (int i = 0; i < 32; ++i) { const int k = k0 + 2 * i + (lane >> 5); float x = v[i] * wscale; if (KS) x *= (k < ksplit ? ksA[k] : ksB[k - ksplit]); scr[(2 * i + (lane >> 5)) * 33 + (lane & 31)] = x; }
;     LDS_WAIT(); asm volatile("" ::: "memory");
;     const int c = lane & 7;
; #pragma unroll
;     for (int j = 0; j < 4; ++j) { const int n = (lane >> 3) + 8 * j; const LAS float* s = scr + (8 * c) * 33 + n;
;         const unsigned long long o = (unsigned long long)pg8::pk4_fp8(s[0 * 33], s[1 * 33], s[2 * 33], s[3 * 33]) | ((unsigned long long)pg8::pk4_fp8(s[4 * 33], s[5 * 33], s[6 * 33], s[7 * 33]) << 32);
;         *(GAS unsigned long long*)(WT + (size_t)(n0 + n) * K + k0 + 8 * c) = o; }
	s_add_i32 s17, s16, 3648
	s_min_u32 s17, s17, 0xfff
	s_lshr_b32 s18, s17, 5
	s_add_i32 s18, s18, 0
	s_and_b32 s19, s17, 31
	s_lshl_b32 s18, s18, 21
	s_lshl_b32 s19, s19, 9
	s_add_u32 s18, s18, s19
	s_add_u32 s12, s2, s18
	s_addc_u32 s13, s3, 0
	global_load_dwordx4 v[100:103], v10, s[12:13]
	s_add_u32 s12, s12, 0x8000
	s_addc_u32 s13, s13, 0
	global_load_dwordx4 v[104:107], v10, s[12:13]
	s_add_u32 s12, s12, 0x8000
	s_addc_u32 s13, s13, 0
	global_load_dwordx4 v[108:111], v10, s[12:13]
	s_add_u32 s12, s12, 0x8000
	s_addc_u32 s13, s13, 0
	global_load_dwordx4 v[112:115], v10, s[12:13]
	s_add_u32 s12, s12, 0x8000
	s_addc_u32 s13, s13, 0
	global_load_dwordx4 v[116:119], v10, s[12:13]
	s_add_u32 s12, s12, 0x8000
	s_addc_u32 s13, s13, 0
	global_load_dwordx4 v[120:123], v10, s[12:13]
	s_add_u32 s12, s12, 0x8000
	s_addc_u32 s13, s13, 0
	global_load_dwordx4 v[124:127], v10, s[12:13]
	s_add_u32 s12, s12, 0x8000
	s_addc_u32 s13, s13, 0
	global_load_dwordx4 v[128:131], v10, s[12:13]
	s_add_i32 s17, s16, 3264
	s_min_u32 s17, s17, 0xfff
	s_lshr_b32 s18, s17, 5
	s_add_i32 s18, s18, 0
	s_and_b32 s19, s17, 31
	s_lshl_b32 s19, s19, 21
	s_lshl_b32 s18, s18, 7
	s_add_u32 s18, s18, s19
	s_add_u32 s14, s4, s18
	s_addc_u32 s15, s5, 0
	ds_read_b32 v170, v6
	ds_read_b32 v171, v6 offset:512
	ds_read_b32 v172, v6 offset:1024
	ds_read_b32 v173, v6 offset:1536
	ds_read_b32 v174, v6 offset:2048
	ds_read_b32 v175, v6 offset:2560
	ds_read_b32 v176, v6 offset:3072
	ds_read_b32 v177, v6 offset:3584
	ds_read_b32 v196, v6 offset:4096
	ds_read_b32 v197, v6 offset:4608
	ds_read_b32 v198, v6 offset:5120
	ds_read_b32 v199, v6 offset:5632
	ds_read_b32 v200, v6 offset:6144
	ds_read_b32 v201, v6 offset:6656
	ds_read_b32 v202, v6 offset:7168
	ds_read_b32 v203, v6 offset:7680
	s_waitcnt lgkmcnt(0)
	v_max_f32_e32 v170, v170, v170
	v_max_f32_e32 v171, v171, v171
	v_max_f32_e32 v172, v172, v172
	v_max_f32_e32 v173, v173, v173
	v_max_f32_e32 v174, v174, v174
	v_max_f32_e32 v175, v175, v175
	v_max_f32_e32 v176, v176, v176
	v_max_f32_e32 v177, v177, v177
	v_max_f32_e32 v196, v196, v196
	v_max_f32_e32 v197, v197, v197
	v_max_f32_e32 v198, v198, v198
	v_max_f32_e32 v199, v199, v199
	v_max_f32_e32 v200, v200, v200
	v_max_f32_e32 v201, v201, v201
	v_max_f32_e32 v202, v202, v202
	v_max_f32_e32 v203, v203, v203
	v_med3_f32 v170, v170, s20, v13
	v_med3_f32 v171, v171, s20, v13
	v_med3_f32 v172, v172, s20, v13
	v_med3_f32 v173, v173, s20, v13
	v_med3_f32 v174, v174, s20, v13
	v_med3_f32 v175, v175, s20, v13
	v_med3_f32 v176, v176, s20, v13
	v_med3_f32 v177, v177, s20, v13
	v_med3_f32 v196, v196, s20, v13
	v_med3_f32 v197, v197, s20, v13
	v_med3_f32 v198, v198, s20, v13
	v_med3_f32 v199, v199, s20, v13
	v_med3_f32 v200, v200, s20, v13
	v_med3_f32 v201, v201, s20, v13
	v_med3_f32 v202, v202, s20, v13
	v_med3_f32 v203, v203, s20, v13
	v_mov_b32_e32 v208, 0
	v_mov_b32_e32 v209, 0
	v_mov_b32_e32 v210, 0
	v_mov_b32_e32 v211, 0
	v_cvt_pk_fp8_f32 v208, v170, v171
	v_cvt_pk_fp8_f32 v209, v174, v175
	v_cvt_pk_fp8_f32 v210, v196, v197
	v_cvt_pk_fp8_f32 v211, v200, v201
	v_cvt_pk_fp8_f32 v208, v172, v173 op_sel:[0,0,1]
	v_cvt_pk_fp8_f32 v209, v176, v177 op_sel:[0,0,1]
	v_cvt_pk_fp8_f32 v210, v198, v199 op_sel:[0,0,1]
	v_cvt_pk_fp8_f32 v211, v202, v203 op_sel:[0,0,1]
	s_nop 0
	global_store_dwordx4 v11, v[208:211], s[14:15]
	ds_read_b32 v170, v8
	ds_read_b32 v171, v8 offset:512
	ds_read_b32 v172, v8 offset:1024
	ds_read_b32 v173, v8 offset:1536
	ds_read_b32 v174, v8 offset:2048
	ds_read_b32 v175, v8 offset:2560
	ds_read_b32 v176, v8 offset:3072
	ds_read_b32 v177, v8 offset:3584
	ds_read_b32 v196, v8 offset:4096
	ds_read_b32 v197, v8 offset:4608
	ds_read_b32 v198, v8 offset:5120
	ds_read_b32 v199, v8 offset:5632
	ds_read_b32 v200, v8 offset:6144
	ds_read_b32 v201, v8 offset:6656
	ds_read_b32 v202, v8 offset:7168
	ds_read_b32 v203, v8 offset:7680
	s_waitcnt lgkmcnt(0)
	v_max_f32_e32 v170, v170, v170
	v_max_f32_e32 v171, v171, v171
	v_max_f32_e32 v172, v172, v172
	v_max_f32_e32 v173, v173, v173
	v_max_f32_e32 v174, v174, v174
	v_max_f32_e32 v175, v175, v175
	v_max_f32_e32 v176, v176, v176
	v_max_f32_e32 v177, v177, v177
	v_max_f32_e32 v196, v196, v196
	v_max_f32_e32 v197, v197, v197
	v_max_f32_e32 v198, v198, v198
	v_max_f32_e32 v199, v199, v199
	v_max_f32_e32 v200, v200, v200
	v_max_f32_e32 v201, v201, v201
	v_max_f32_e32 v202, v202, v202
	v_max_f32_e32 v203, v203, v203
	v_med3_f32 v170, v170, s20, v13
	v_med3_f32 v171, v171, s20, v13
	v_med3_f32 v172, v172, s20, v13
	v_med3_f32 v173, v173, s20, v13
	v_med3_f32 v174, v174, s20, v13
	v_med3_f32 v175, v175, s20, v13
	v_med3_f32 v176, v176, s20, v13
	v_med3_f32 v177, v177, s20, v13
	v_med3_f32 v196, v196, s20, v13
	v_med3_f32 v197, v197, s20, v13
	v_med3_f32 v198, v198, s20, v13
	v_med3_f32 v199, v199, s20, v13
	v_med3_f32 v200, v200, s20, v13
	v_med3_f32 v201, v201, s20, v13
	v_med3_f32 v202, v202, s20, v13
	v_med3_f32 v203, v203, s20, v13
	v_mov_b32_e32 v208, 0
	v_mov_b32_e32 v209, 0
	v_mov_b32_e32 v210, 0
	v_mov_b32_e32 v211, 0
	v_cvt_pk_fp8_f32 v208, v170, v171
	v_cvt_pk_fp8_f32 v209, v174, v175
	v_cvt_pk_fp8_f32 v210, v196, v197
	v_cvt_pk_fp8_f32 v211, v200, v201
	v_cvt_pk_fp8_f32 v208, v172, v173 op_sel:[0,0,1]
	v_cvt_pk_fp8_f32 v209, v176, v177 op_sel:[0,0,1]
	v_cvt_pk_fp8_f32 v210, v198, v199 op_sel:[0,0,1]
	v_cvt_pk_fp8_f32 v211, v202, v203 op_sel:[0,0,1]
	s_nop 0
	global_store_dwordx4 v12, v[208:211], s[14:15]
	s_waitcnt vmcnt(32)
	v_mul_f32_e32 v132, 0x43000000, v132
	v_mul_f32_e32 v133, 0x43000000, v133
	v_mul_f32_e32 v134, 0x43000000, v134
	v_mul_f32_e32 v135, 0x43000000, v135
	ds_write_b128 v5, v[132:135]
	v_mul_f32_e32 v136, 0x43000000, v136
	v_mul_f32_e32 v137, 0x43000000, v137
	v_mul_f32_e32 v138, 0x43000000, v138
	v_mul_f32_e32 v139, 0x43000000, v139
	ds_write_b128 v5, v[136:139] offset:1024
	v_mul_f32_e32 v140, 0x43000000, v140
	v_mul_f32_e32 v141, 0x43000000, v141
	v_mul_f32_e32 v142, 0x43000000, v142
	v_mul_f32_e32 v143, 0x43000000, v143
	ds_write_b128 v5, v[140:143] offset:2048
	v_mul_f32_e32 v144, 0x43000000, v144
	v_mul_f32_e32 v145, 0x43000000, v145
	v_mul_f32_e32 v146, 0x43000000, v146
	v_mul_f32_e32 v147, 0x43000000, v147
	ds_write_b128 v5, v[144:147] offset:3072
	v_mul_f32_e32 v148, 0x43000000, v148
	v_mul_f32_e32 v149, 0x43000000, v149
	v_mul_f32_e32 v150, 0x43000000, v150
	v_mul_f32_e32 v151, 0x43000000, v151
	ds_write_b128 v5, v[148:151] offset:4096
	v_mul_f32_e32 v152, 0x43000000, v152
	v_mul_f32_e32 v153, 0x43000000, v153
	v_mul_f32_e32 v154, 0x43000000, v154
	v_mul_f32_e32 v155, 0x43000000, v155
	ds_write_b128 v5, v[152:155] offset:5120
	v_mul_f32_e32 v156, 0x43000000, v156
	v_mul_f32_e32 v157, 0x43000000, v157
	v_mul_f32_e32 v158, 0x43000000, v158
	v_mul_f32_e32 v159, 0x43000000, v159
	ds_write_b128 v5, v[156:159] offset:6144
	v_mul_f32_e32 v160, 0x43000000, v160
	v_mul_f32_e32 v161, 0x43000000, v161
	v_mul_f32_e32 v162, 0x43000000, v162
	v_mul_f32_e32 v163, 0x43000000, v163
	ds_write_b128 v5, v[160:163] offset:7168
	s_waitcnt lgkmcnt(0)
	s_barrier
; #define GAS __attribute__((address_space(1)))
; #define LAS __attribute__((address_space(3)))
; #define LDS_WAIT() asm volatile("s_waitcnt lgkmcnt(0)" ::: "memory")
; __device__ __forceinline__ unsigned pk4_fp8(float a, float b, float c, float d) {
;     a = fminf(fmaxf(a, -448.f), 448.f); b = fminf(fmaxf(b, -448.f), 448.f); c = fminf(fmaxf(c, -448.f), 448.f); d = fminf(fmaxf(d, -448.f), 448.f);
;     int w = __builtin_amdgcn_cvt_pk_fp8_f32(a, b, 0, false); w = __builtin_amdgcn_cvt_pk_fp8_f32(c, d, w, true); return (unsigned)w; }
;     ...
; #pragma unroll
;     for (int i = 0; i < 32; ++i) v[i] = sc >= 0 ? W[(size_t)(k0 + 2 * i + (lane >> 5)) * Nsrc + sc] : 0.f;
; #pragma unroll
;     for (int i = 0; i < 32; ++i) { const int k = k0 + 2 * i + (lane >> 5); float x = v[i] * wscale; if (KS) x *= (k < ksplit ? ksA[k] : ksB[k - ksplit]); scr[(2 * i + (lane >> 5)) * 33 + (lane & 31)] = x; }
;     LDS_WAIT(); asm volatile("" ::: "memory");
;     const int c = lane & 7;
; #pragma unroll
;     for (int j = 0; j < 4; ++j) { const int n = (lane >> 3) + 8 * j; const LAS float* s = scr + (8 * c) * 33 + n;
;         const unsigned long long o = (unsigned long long)pg8::pk4_fp8(s[0 * 33], s[1 * 33], s[2 * 33], s[3 * 33]) | ((unsigned long long)pg8::pk4_fp8(s[4 * 33], s[5 * 33], s[6 * 33], s[7 * 33]) << 32);
;         *(GAS unsigned long long*)(WT + (size_t)(n0 + n) * K + k0 + 8 * c) = o; }
	s_add_i32 s17, s16, 3744
	s_min_u32 s17, s17, 0xfff
	s_lshr_b32 s18, s17, 5
	s_add_i32 s18, s18, 0
	s_and_b32 s19, s17, 31
	s_lshl_b32 s18, s18, 21
	s_lshl_b32 s19, s19, 9
	s_add_u32 s18, s18, s19
	s_add_u32 s12, s2, s18
	s_addc_u32 s13, s3, 0
	global_load_dwordx4 v[132:135], v10, s[12:13]
	s_add_u32 s12, s12, 0x8000
	s_addc_u32 s13, s13, 0
	global_load_dwordx4 v[136:139], v10, s[12:13]
	s_add_u32 s12, s12, 0x8000
	s_addc_u32 s13, s13, 0
	global_load_dwordx4 v[140:143], v10, s[12:13]
	s_add_u32 s12, s12, 0x8000
	s_addc_u32 s13, s13, 0
	global_load_dwordx4 v[144:147], v10, s[12:13]
	s_add_u32 s12, s12, 0x8000
	s_addc_u32 s13, s13, 0
	global_load_dwordx4 v[148:151], v10, s[12:13]
	s_add_u32 s12, s12, 0x8000
	s_addc_u32 s13, s13, 0
	global_load_dwordx4 v[152:155], v10, s[12:13]
	s_add_u32 s12, s12, 0x8000
	s_addc_u32 s13, s13, 0
	global_load_dwordx4 v[156:159], v10, s[12:13]
	s_add_u32 s12, s12, 0x8000
	s_addc_u32 s13, s13, 0
	global_load_dwordx4 v[160:163], v10, s[12:13]
	s_add_i32 s17, s16, 3360
	s_min_u32 s17, s17, 0xfff
	s_lshr_b32 s18, s17, 5
	s_add_i32 s18, s18, 0
	s_and_b32 s19, s17, 31
	s_lshl_b32 s19, s19, 21
	s_lshl_b32 s18, s18, 7
	s_add_u32 s18, s18, s19
	s_add_u32 s14, s4, s18
	s_addc_u32 s15, s5, 0
	ds_read_b32 v170, v7
	ds_read_b32 v171, v7 offset:512
	ds_read_b32 v172, v7 offset:1024
	ds_read_b32 v173, v7 offset:1536
	ds_read_b32 v174, v7 offset:2048
	ds_read_b32 v175, v7 offset:2560
	ds_read_b32 v176, v7 offset:3072
	ds_read_b32 v177, v7 offset:3584
	ds_read_b32 v196, v7 offset:4096
	ds_read_b32 v197, v7 offset:4608
	ds_read_b32 v198, v7 offset:5120
	ds_read_b32 v199, v7 offset:5632
	ds_read_b32 v200, v7 offset:6144
	ds_read_b32 v201, v7 offset:6656
	ds_read_b32 v202, v7 offset:7168
	ds_read_b32 v203, v7 offset:7680
	s_waitcnt lgkmcnt(0)
	v_max_f32_e32 v170, v170, v170
	v_max_f32_e32 v171, v171, v171
	v_max_f32_e32 v172, v172, v172
	v_max_f32_e32 v173, v173, v173
	v_max_f32_e32 v174, v174, v174
	v_max_f32_e32 v175, v175, v175
	v_max_f32_e32 v176, v176, v176
	v_max_f32_e32 v177, v177, v177
	v_max_f32_e32 v196, v196, v196
	v_max_f32_e32 v197, v197, v197
	v_max_f32_e32 v198, v198, v198
	v_max_f32_e32 v199, v199, v199
	v_max_f32_e32 v200, v200, v200
	v_max_f32_e32 v201, v201, v201
	v_max_f32_e32 v202, v202, v202
	v_max_f32_e32 v203, v203, v203
	v_med3_f32 v170, v170, s20, v13
	v_med3_f32 v171, v171, s20, v13
	v_med3_f32 v172, v172, s20, v13
	v_med3_f32 v173, v173, s20, v13
	v_med3_f32 v174, v174, s20, v13
	v_med3_f32 v175, v175, s20, v13
	v_med3_f32 v176, v176, s20, v13
	v_med3_f32 v177, v177, s20, v13
	v_med3_f32 v196, v196, s20, v13
	v_med3_f32 v197, v197, s20, v13
	v_med3_f32 v198, v198, s20, v13
	v_med3_f32 v199, v199, s20, v13
	v_med3_f32 v200, v200, s20, v13
	v_med3_f32 v201, v201, s20, v13
	v_med3_f32 v202, v202, s20, v13
	v_med3_f32 v203, v203, s20, v13
	v_mov_b32_e32 v208, 0
	v_mov_b32_e32 v209, 0
	v_mov_b32_e32 v210, 0
	v_mov_b32_e32 v211, 0
	v_cvt_pk_fp8_f32 v208, v170, v171
	v_cvt_pk_fp8_f32 v209, v174, v175
	v_cvt_pk_fp8_f32 v210, v196, v197
	v_cvt_pk_fp8_f32 v211, v200, v201
	v_cvt_pk_fp8_f32 v208, v172, v173 op_sel:[0,0,1]
	v_cvt_pk_fp8_f32 v209, v176, v177 op_sel:[0,0,1]
	v_cvt_pk_fp8_f32 v210, v198, v199 op_sel:[0,0,1]
	v_cvt_pk_fp8_f32 v211, v202, v203 op_sel:[0,0,1]
	s_nop 0
	global_store_dwordx4 v11, v[208:211], s[14:15]
	ds_read_b32 v170, v9
	ds_read_b32 v171, v9 offset:512
	ds_read_b32 v172, v9 offset:1024
	ds_read_b32 v173, v9 offset:1536
	ds_read_b32 v174, v9 offset:2048
	ds_read_b32 v175, v9 offset:2560
	ds_read_b32 v176, v9 offset:3072
	ds_read_b32 v177, v9 offset:3584
	ds_read_b32 v196, v9 offset:4096
	ds_read_b32 v197, v9 offset:4608
	ds_read_b32 v198, v9 offset:5120
	ds_read_b32 v199, v9 offset:5632
	ds_read_b32 v200, v9 offset:6144
	ds_read_b32 v201, v9 offset:6656
	ds_read_b32 v202, v9 offset:7168
	ds_read_b32 v203, v9 offset:7680
	s_waitcnt lgkmcnt(0)
	v_max_f32_e32 v170, v170, v170
	v_max_f32_e32 v171, v171, v171
	v_max_f32_e32 v172, v172, v172
	v_max_f32_e32 v173, v173, v173
	v_max_f32_e32 v174, v174, v174
	v_max_f32_e32 v175, v175, v175
	v_max_f32_e32 v176, v176, v176
	v_max_f32_e32 v177, v177, v177
	v_max_f32_e32 v196, v196, v196
	v_max_f32_e32 v197, v197, v197
	v_max_f32_e32 v198, v198, v198
	v_max_f32_e32 v199, v199, v199
	v_max_f32_e32 v200, v200, v200
	v_max_f32_e32 v201, v201, v201
	v_max_f32_e32 v202, v202, v202
	v_max_f32_e32 v203, v203, v203
	v_med3_f32 v170, v170, s20, v13
	v_med3_f32 v171, v171, s20, v13
	v_med3_f32 v172, v172, s20, v13
	v_med3_f32 v173, v173, s20, v13
	v_med3_f32 v174, v174, s20, v13
	v_med3_f32 v175, v175, s20, v13
	v_med3_f32 v176, v176, s20, v13
	v_med3_f32 v177, v177, s20, v13
	v_med3_f32 v196, v196, s20, v13
	v_med3_f32 v197, v197, s20, v13
	v_med3_f32 v198, v198, s20, v13
	v_med3_f32 v199, v199, s20, v13
	v_med3_f32 v200, v200, s20, v13
	v_med3_f32 v201, v201, s20, v13
	v_med3_f32 v202, v202, s20, v13
	v_med3_f32 v203, v203, s20, v13
	v_mov_b32_e32 v208, 0
	v_mov_b32_e32 v209, 0
	v_mov_b32_e32 v210, 0
	v_mov_b32_e32 v211, 0
	v_cvt_pk_fp8_f32 v208, v170, v171
	v_cvt_pk_fp8_f32 v209, v174, v175
	v_cvt_pk_fp8_f32 v210, v196, v197
	v_cvt_pk_fp8_f32 v211, v200, v201
	v_cvt_pk_fp8_f32 v208, v172, v173 op_sel:[0,0,1]
	v_cvt_pk_fp8_f32 v209, v176, v177 op_sel:[0,0,1]
	v_cvt_pk_fp8_f32 v210, v198, v199 op_sel:[0,0,1]
	v_cvt_pk_fp8_f32 v211, v202, v203 op_sel:[0,0,1]
	s_nop 0
	global_store_dwordx4 v12, v[208:211], s[14:15]
	s_waitcnt vmcnt(32)
	v_mul_f32_e32 v36, 0x43000000, v36
	v_mul_f32_e32 v37, 0x43000000, v37
	v_mul_f32_e32 v38, 0x43000000, v38
	v_mul_f32_e32 v39, 0x43000000, v39
	ds_write_b128 v4, v[36:39]
	v_mul_f32_e32 v40, 0x43000000, v40
	v_mul_f32_e32 v41, 0x43000000, v41
	v_mul_f32_e32 v42, 0x43000000, v42
	v_mul_f32_e32 v43, 0x43000000, v43
	ds_write_b128 v4, v[40:43] offset:1024
	v_mul_f32_e32 v44, 0x43000000, v44
	v_mul_f32_e32 v45, 0x43000000, v45
	v_mul_f32_e32 v46, 0x43000000, v46
	v_mul_f32_e32 v47, 0x43000000, v47
	ds_write_b128 v4, v[44:47] offset:2048
	v_mul_f32_e32 v48, 0x43000000, v48
	v_mul_f32_e32 v49, 0x43000000, v49
	v_mul_f32_e32 v50, 0x43000000, v50
	v_mul_f32_e32 v51, 0x43000000, v51
	ds_write_b128 v4, v[48:51] offset:3072
	v_mul_f32_e32 v52, 0x43000000, v52
	v_mul_f32_e32 v53, 0x43000000, v53
	v_mul_f32_e32 v54, 0x43000000, v54
	v_mul_f32_e32 v55, 0x43000000, v55
	ds_write_b128 v4, v[52:55] offset:4096
	v_mul_f32_e32 v56, 0x43000000, v56
	v_mul_f32_e32 v57, 0x43000000, v57
	v_mul_f32_e32 v58, 0x43000000, v58
	v_mul_f32_e32 v59, 0x43000000, v59
	ds_write_b128 v4, v[56:59] offset:5120
	v_mul_f32_e32 v60, 0x43000000, v60
	v_mul_f32_e32 v61, 0x43000000, v61
	v_mul_f32_e32 v62, 0x43000000, v62
	v_mul_f32_e32 v63, 0x43000000, v63
	ds_write_b128 v4, v[60:63] offset:6144
	v_mul_f32_e32 v64, 0x43000000, v64
	v_mul_f32_e32 v65, 0x43000000, v65
	v_mul_f32_e32 v66, 0x43000000, v66
	v_mul_f32_e32 v67, 0x43000000, v67
	ds_write_b128 v4, v[64:67] offset:7168
	s_waitcnt lgkmcnt(0)
	s_barrier
; #define GAS __attribute__((address_space(1)))
; #define LAS __attribute__((address_space(3)))
; #define LDS_WAIT() asm volatile("s_waitcnt lgkmcnt(0)" ::: "memory")
; __device__ __forceinline__ unsigned pk4_fp8(float a, float b, float c, float d) {
;     a = fminf(fmaxf(a, -448.f), 448.f); b = fminf(fmaxf(b, -448.f), 448.f); c = fminf(fmaxf(c, -448.f), 448.f); d = fminf(fmaxf(d, -448.f), 448.f);
;     int w = __builtin_amdgcn_cvt_pk_fp8_f32(a, b, 0, false); w = __builtin_amdgcn_cvt_pk_fp8_f32(c, d, w, true); return (unsigned)w; }
;     ...
; #pragma unroll
;     for (int i = 0; i < 32; ++i) v[i] = sc >= 0 ? W[(size_t)(k0 + 2 * i + (lane >> 5)) * Nsrc + sc] : 0.f;
; #pragma unroll
;     for (int i = 0; i < 32; ++i) { const int k = k0 + 2 * i + (lane >> 5); float x = v[i] * wscale; if (KS) x *= (k < ksplit ? ksA[k] : ksB[k - ksplit]); scr[(2 * i + (lane >> 5)) * 33 + (lane & 31)] = x; }
;     LDS_WAIT(); asm volatile("" ::: "memory");
;     const int c = lane & 7;
; #pragma unroll
;     for (int j = 0; j < 4; ++j) { const int n = (lane >> 3) + 8 * j; const LAS float* s = scr + (8 * c) * 33 + n;
;         const unsigned long long o = (unsigned long long)pg8::pk4_fp8(s[0 * 33], s[1 * 33], s[2 * 33], s[3 * 33]) | ((unsigned long long)pg8::pk4_fp8(s[4 * 33], s[5 * 33], s[6 * 33], s[7 * 33]) << 32);
;         *(GAS unsigned long long*)(WT + (size_t)(n0 + n) * K + k0 + 8 * c) = o; }
	s_add_i32 s17, s16, 3840
	s_min_u32 s17, s17, 0xfff
	s_lshr_b32 s18, s17, 5
	s_add_i32 s18, s18, 0
	s_and_b32 s19, s17, 31
	s_lshl_b32 s18, s18, 21
	s_lshl_b32 s19, s19, 9
	s_add_u32 s18, s18, s19
	s_add_u32 s12, s2, s18
	s_addc_u32 s13, s3, 0
	global_load_dwordx4 v[36:39], v10, s[12:13]
	s_add_u32 s12, s12, 0x8000
	s_addc_u32 s13, s13, 0
	global_load_dwordx4 v[40:43], v10, s[12:13]
	s_add_u32 s12, s12, 0x8000
	s_addc_u32 s13, s13, 0
	global_load_dwordx4 v[44:47], v10, s[12:13]
	s_add_u32 s12, s12, 0x8000
	s_addc_u32 s13, s13, 0
	global_load_dwordx4 v[48:51], v10, s[12:13]
	s_add_u32 s12, s12, 0x8000
	s_addc_u32 s13, s13, 0
	global_load_dwordx4 v[52:55], v10, s[12:13]
	s_add_u32 s12, s12, 0x8000
	s_addc_u32 s13, s13, 0
	global_load_dwordx4 v[56:59], v10, s[12:13]
	s_add_u32 s12, s12, 0x8000
	s_addc_u32 s13, s13, 0
	global_load_dwordx4 v[60:63], v10, s[12:13]
	s_add_u32 s12, s12, 0x8000
	s_addc_u32 s13, s13, 0
	global_load_dwordx4 v[64:67], v10, s[12:13]
	s_add_i32 s17, s16, 3456
	s_min_u32 s17, s17, 0xfff
	s_lshr_b32 s18, s17, 5
	s_add_i32 s18, s18, 0
	s_and_b32 s19, s17, 31
	s_lshl_b32 s19, s19, 21
	s_lshl_b32 s18, s18, 7
	s_add_u32 s18, s18, s19
	s_add_u32 s14, s4, s18
	s_addc_u32 s15, s5, 0
	ds_read_b32 v170, v6
	ds_read_b32 v171, v6 offset:512
	ds_read_b32 v172, v6 offset:1024
	ds_read_b32 v173, v6 offset:1536
	ds_read_b32 v174, v6 offset:2048
	ds_read_b32 v175, v6 offset:2560
	ds_read_b32 v176, v6 offset:3072
	ds_read_b32 v177, v6 offset:3584
	ds_read_b32 v196, v6 offset:4096
	ds_read_b32 v197, v6 offset:4608
	ds_read_b32 v198, v6 offset:5120
	ds_read_b32 v199, v6 offset:5632
	ds_read_b32 v200, v6 offset:6144
	ds_read_b32 v201, v6 offset:6656
	ds_read_b32 v202, v6 offset:7168
	ds_read_b32 v203, v6 offset:7680
	s_waitcnt lgkmcnt(0)
	v_max_f32_e32 v170, v170, v170
	v_max_f32_e32 v171, v171, v171
	v_max_f32_e32 v172, v172, v172
	v_max_f32_e32 v173, v173, v173
	v_max_f32_e32 v174, v174, v174
	v_max_f32_e32 v175, v175, v175
	v_max_f32_e32 v176, v176, v176
	v_max_f32_e32 v177, v177, v177
	v_max_f32_e32 v196, v196, v196
	v_max_f32_e32 v197, v197, v197
	v_max_f32_e32 v198, v198, v198
	v_max_f32_e32 v199, v199, v199
	v_max_f32_e32 v200, v200, v200
	v_max_f32_e32 v201, v201, v201
	v_max_f32_e32 v202, v202, v202
	v_max_f32_e32 v203, v203, v203
	v_med3_f32 v170, v170, s20, v13
	v_med3_f32 v171, v171, s20, v13
	v_med3_f32 v172, v172, s20, v13
	v_med3_f32 v173, v173, s20, v13
	v_med3_f32 v174, v174, s20, v13
	v_med3_f32 v175, v175, s20, v13
	v_med3_f32 v176, v176, s20, v13
	v_med3_f32 v177, v177, s20, v13
	v_med3_f32 v196, v196, s20, v13
	v_med3_f32 v197, v197, s20, v13
	v_med3_f32 v198, v198, s20, v13
	v_med3_f32 v199, v199, s20, v13
	v_med3_f32 v200, v200, s20, v13
	v_med3_f32 v201, v201, s20, v13
	v_med3_f32 v202, v202, s20, v13
	v_med3_f32 v203, v203, s20, v13
	v_mov_b32_e32 v208, 0
	v_mov_b32_e32 v209, 0
	v_mov_b32_e32 v210, 0
	v_mov_b32_e32 v211, 0
	v_cvt_pk_fp8_f32 v208, v170, v171
	v_cvt_pk_fp8_f32 v209, v174, v175
	v_cvt_pk_fp8_f32 v210, v196, v197
	v_cvt_pk_fp8_f32 v211, v200, v201
	v_cvt_pk_fp8_f32 v208, v172, v173 op_sel:[0,0,1]
	v_cvt_pk_fp8_f32 v209, v176, v177 op_sel:[0,0,1]
	v_cvt_pk_fp8_f32 v210, v198, v199 op_sel:[0,0,1]
	v_cvt_pk_fp8_f32 v211, v202, v203 op_sel:[0,0,1]
	s_nop 0
	global_store_dwordx4 v11, v[208:211], s[14:15]
	ds_read_b32 v170, v8
	ds_read_b32 v171, v8 offset:512
	ds_read_b32 v172, v8 offset:1024
	ds_read_b32 v173, v8 offset:1536
	ds_read_b32 v174, v8 offset:2048
	ds_read_b32 v175, v8 offset:2560
	ds_read_b32 v176, v8 offset:3072
	ds_read_b32 v177, v8 offset:3584
	ds_read_b32 v196, v8 offset:4096
	ds_read_b32 v197, v8 offset:4608
	ds_read_b32 v198, v8 offset:5120
	ds_read_b32 v199, v8 offset:5632
	ds_read_b32 v200, v8 offset:6144
	ds_read_b32 v201, v8 offset:6656
	ds_read_b32 v202, v8 offset:7168
	ds_read_b32 v203, v8 offset:7680
	s_waitcnt lgkmcnt(0)
	v_max_f32_e32 v170, v170, v170
	v_max_f32_e32 v171, v171, v171
	v_max_f32_e32 v172, v172, v172
	v_max_f32_e32 v173, v173, v173
	v_max_f32_e32 v174, v174, v174
	v_max_f32_e32 v175, v175, v175
	v_max_f32_e32 v176, v176, v176
	v_max_f32_e32 v177, v177, v177
	v_max_f32_e32 v196, v196, v196
	v_max_f32_e32 v197, v197, v197
	v_max_f32_e32 v198, v198, v198
	v_max_f32_e32 v199, v199, v199
	v_max_f32_e32 v200, v200, v200
	v_max_f32_e32 v201, v201, v201
	v_max_f32_e32 v202, v202, v202
	v_max_f32_e32 v203, v203, v203
	v_med3_f32 v170, v170, s20, v13
	v_med3_f32 v171, v171, s20, v13
	v_med3_f32 v172, v172, s20, v13
	v_med3_f32 v173, v173, s20, v13
	v_med3_f32 v174, v174, s20, v13
	v_med3_f32 v175, v175, s20, v13
	v_med3_f32 v176, v176, s20, v13
	v_med3_f32 v177, v177, s20, v13
	v_med3_f32 v196, v196, s20, v13
	v_med3_f32 v197, v197, s20, v13
	v_med3_f32 v198, v198, s20, v13
	v_med3_f32 v199, v199, s20, v13
	v_med3_f32 v200, v200, s20, v13
	v_med3_f32 v201, v201, s20, v13
	v_med3_f32 v202, v202, s20, v13
	v_med3_f32 v203, v203, s20, v13
	v_mov_b32_e32 v208, 0
	v_mov_b32_e32 v209, 0
	v_mov_b32_e32 v210, 0
	v_mov_b32_e32 v211, 0
	v_cvt_pk_fp8_f32 v208, v170, v171
	v_cvt_pk_fp8_f32 v209, v174, v175
	v_cvt_pk_fp8_f32 v210, v196, v197
	v_cvt_pk_fp8_f32 v211, v200, v201
	v_cvt_pk_fp8_f32 v208, v172, v173 op_sel:[0,0,1]
	v_cvt_pk_fp8_f32 v209, v176, v177 op_sel:[0,0,1]
	v_cvt_pk_fp8_f32 v210, v198, v199 op_sel:[0,0,1]
	v_cvt_pk_fp8_f32 v211, v202, v203 op_sel:[0,0,1]
	s_nop 0
	global_store_dwordx4 v12, v[208:211], s[14:15]
	s_waitcnt vmcnt(32)
	v_mul_f32_e32 v68, 0x43000000, v68
	v_mul_f32_e32 v69, 0x43000000, v69
	v_mul_f32_e32 v70, 0x43000000, v70
	v_mul_f32_e32 v71, 0x43000000, v71
	ds_write_b128 v5, v[68:71]
	v_mul_f32_e32 v72, 0x43000000, v72
	v_mul_f32_e32 v73, 0x43000000, v73
	v_mul_f32_e32 v74, 0x43000000, v74
	v_mul_f32_e32 v75, 0x43000000, v75
	ds_write_b128 v5, v[72:75] offset:1024
	v_mul_f32_e32 v76, 0x43000000, v76
	v_mul_f32_e32 v77, 0x43000000, v77
	v_mul_f32_e32 v78, 0x43000000, v78
	v_mul_f32_e32 v79, 0x43000000, v79
	ds_write_b128 v5, v[76:79] offset:2048
	v_mul_f32_e32 v80, 0x43000000, v80
	v_mul_f32_e32 v81, 0x43000000, v81
	v_mul_f32_e32 v82, 0x43000000, v82
	v_mul_f32_e32 v83, 0x43000000, v83
	ds_write_b128 v5, v[80:83] offset:3072
	v_mul_f32_e32 v84, 0x43000000, v84
	v_mul_f32_e32 v85, 0x43000000, v85
	v_mul_f32_e32 v86, 0x43000000, v86
	v_mul_f32_e32 v87, 0x43000000, v87
	ds_write_b128 v5, v[84:87] offset:4096
	v_mul_f32_e32 v88, 0x43000000, v88
	v_mul_f32_e32 v89, 0x43000000, v89
	v_mul_f32_e32 v90, 0x43000000, v90
	v_mul_f32_e32 v91, 0x43000000, v91
	ds_write_b128 v5, v[88:91] offset:5120
	v_mul_f32_e32 v92, 0x43000000, v92
	v_mul_f32_e32 v93, 0x43000000, v93
	v_mul_f32_e32 v94, 0x43000000, v94
	v_mul_f32_e32 v95, 0x43000000, v95
	ds_write_b128 v5, v[92:95] offset:6144
	v_mul_f32_e32 v96, 0x43000000, v96
	v_mul_f32_e32 v97, 0x43000000, v97
	v_mul_f32_e32 v98, 0x43000000, v98
	v_mul_f32_e32 v99, 0x43000000, v99
	ds_write_b128 v5, v[96:99] offset:7168
	s_waitcnt lgkmcnt(0)
	s_barrier
; #define GAS __attribute__((address_space(1)))
; #define LAS __attribute__((address_space(3)))
; #define LDS_WAIT() asm volatile("s_waitcnt lgkmcnt(0)" ::: "memory")
; __device__ __forceinline__ unsigned pk4_fp8(float a, float b, float c, float d) {
;     a = fminf(fmaxf(a, -448.f), 448.f); b = fminf(fmaxf(b, -448.f), 448.f); c = fminf(fmaxf(c, -448.f), 448.f); d = fminf(fmaxf(d, -448.f), 448.f);
;     int w = __builtin_amdgcn_cvt_pk_fp8_f32(a, b, 0, false); w = __builtin_amdgcn_cvt_pk_fp8_f32(c, d, w, true); return (unsigned)w; }
;     ...
; #pragma unroll
;     for (int i = 0; i < 32; ++i) v[i] = sc >= 0 ? W[(size_t)(k0 + 2 * i + (lane >> 5)) * Nsrc + sc] : 0.f;
; #pragma unroll
;     for (int i = 0; i < 32; ++i) { const int k = k0 + 2 * i + (lane >> 5); float x = v[i] * wscale; if (KS) x *= (k < ksplit ? ksA[k] : ksB[k - ksplit]); scr[(2 * i + (lane >> 5)) * 33 + (lane & 31)] = x; }
;     LDS_WAIT(); asm volatile("" ::: "memory");
;     const int c = lane & 7;
; #pragma unroll
;     for (int j = 0; j < 4; ++j) { const int n = (lane >> 3) + 8 * j; const LAS float* s = scr + (8 * c) * 33 + n;
;         const unsigned long long o = (unsigned long long)pg8::pk4_fp8(s[0 * 33], s[1 * 33], s[2 * 33], s[3 * 33]) | ((unsigned long long)pg8::pk4_fp8(s[4 * 33], s[5 * 33], s[6 * 33], s[7 * 33]) << 32);
;         *(GAS unsigned long long*)(WT + (size_t)(n0 + n) * K + k0 + 8 * c) = o; }
	s_add_i32 s17, s16, 3936
	s_min_u32 s17, s17, 0xfff
	s_lshr_b32 s18, s17, 5
	s_add_i32 s18, s18, 0
	s_and_b32 s19, s17, 31
	s_lshl_b32 s18, s18, 21
	s_lshl_b32 s19, s19, 9
	s_add_u32 s18, s18, s19
	s_add_u32 s12, s2, s18
	s_addc_u32 s13, s3, 0
	global_load_dwordx4 v[68:71], v10, s[12:13]
	s_add_u32 s12, s12, 0x8000
	s_addc_u32 s13, s13, 0
	global_load_dwordx4 v[72:75], v10, s[12:13]
	s_add_u32 s12, s12, 0x8000
	s_addc_u32 s13, s13, 0
	global_load_dwordx4 v[76:79], v10, s[12:13]
	s_add_u32 s12, s12, 0x8000
	s_addc_u32 s13, s13, 0
	global_load_dwordx4 v[80:83], v10, s[12:13]
	s_add_u32 s12, s12, 0x8000
	s_addc_u32 s13, s13, 0
	global_load_dwordx4 v[84:87], v10, s[12:13]
	s_add_u32 s12, s12, 0x8000
	s_addc_u32 s13, s13, 0
	global_load_dwordx4 v[88:91], v10, s[12:13]
	s_add_u32 s12, s12, 0x8000
	s_addc_u32 s13, s13, 0
	global_load_dwordx4 v[92:95], v10, s[12:13]
	s_add_u32 s12, s12, 0x8000
	s_addc_u32 s13, s13, 0
	global_load_dwordx4 v[96:99], v10, s[12:13]
	s_add_i32 s17, s16, 3552
	s_min_u32 s17, s17, 0xfff
	s_lshr_b32 s18, s17, 5
	s_add_i32 s18, s18, 0
	s_and_b32 s19, s17, 31
	s_lshl_b32 s19, s19, 21
	s_lshl_b32 s18, s18, 7
	s_add_u32 s18, s18, s19
	s_add_u32 s14, s4, s18
	s_addc_u32 s15, s5, 0
	ds_read_b32 v170, v7
	ds_read_b32 v171, v7 offset:512
	ds_read_b32 v172, v7 offset:1024
	ds_read_b32 v173, v7 offset:1536
	ds_read_b32 v174, v7 offset:2048
	ds_read_b32 v175, v7 offset:2560
	ds_read_b32 v176, v7 offset:3072
	ds_read_b32 v177, v7 offset:3584
	ds_read_b32 v196, v7 offset:4096
	ds_read_b32 v197, v7 offset:4608
	ds_read_b32 v198, v7 offset:5120
	ds_read_b32 v199, v7 offset:5632
	ds_read_b32 v200, v7 offset:6144
	ds_read_b32 v201, v7 offset:6656
	ds_read_b32 v202, v7 offset:7168
	ds_read_b32 v203, v7 offset:7680
	s_waitcnt lgkmcnt(0)
	v_max_f32_e32 v170, v170, v170
	v_max_f32_e32 v171, v171, v171
	v_max_f32_e32 v172, v172, v172
	v_max_f32_e32 v173, v173, v173
	v_max_f32_e32 v174, v174, v174
	v_max_f32_e32 v175, v175, v175
	v_max_f32_e32 v176, v176, v176
	v_max_f32_e32 v177, v177, v177
	v_max_f32_e32 v196, v196, v196
	v_max_f32_e32 v197, v197, v197
	v_max_f32_e32 v198, v198, v198
	v_max_f32_e32 v199, v199, v199
	v_max_f32_e32 v200, v200, v200
	v_max_f32_e32 v201, v201, v201
	v_max_f32_e32 v202, v202, v202
	v_max_f32_e32 v203, v203, v203
	v_med3_f32 v170, v170, s20, v13
	v_med3_f32 v171, v171, s20, v13
	v_med3_f32 v172, v172, s20, v13
	v_med3_f32 v173, v173, s20, v13
	v_med3_f32 v174, v174, s20, v13
	v_med3_f32 v175, v175, s20, v13
	v_med3_f32 v176, v176, s20, v13
	v_med3_f32 v177, v177, s20, v13
	v_med3_f32 v196, v196, s20, v13
	v_med3_f32 v197, v197, s20, v13
	v_med3_f32 v198, v198, s20, v13
	v_med3_f32 v199, v199, s20, v13
	v_med3_f32 v200, v200, s20, v13
	v_med3_f32 v201, v201, s20, v13
	v_med3_f32 v202, v202, s20, v13
	v_med3_f32 v203, v203, s20, v13
	v_mov_b32_e32 v208, 0
	v_mov_b32_e32 v209, 0
	v_mov_b32_e32 v210, 0
	v_mov_b32_e32 v211, 0
	v_cvt_pk_fp8_f32 v208, v170, v171
	v_cvt_pk_fp8_f32 v209, v174, v175
	v_cvt_pk_fp8_f32 v210, v196, v197
	v_cvt_pk_fp8_f32 v211, v200, v201
	v_cvt_pk_fp8_f32 v208, v172, v173 op_sel:[0,0,1]
	v_cvt_pk_fp8_f32 v209, v176, v177 op_sel:[0,0,1]
	v_cvt_pk_fp8_f32 v210, v198, v199 op_sel:[0,0,1]
	v_cvt_pk_fp8_f32 v211, v202, v203 op_sel:[0,0,1]
	s_nop 0
	global_store_dwordx4 v11, v[208:211], s[14:15]
	ds_read_b32 v170, v9
	ds_read_b32 v171, v9 offset:512
	ds_read_b32 v172, v9 offset:1024
	ds_read_b32 v173, v9 offset:1536
	ds_read_b32 v174, v9 offset:2048
	ds_read_b32 v175, v9 offset:2560
	ds_read_b32 v176, v9 offset:3072
	ds_read_b32 v177, v9 offset:3584
	ds_read_b32 v196, v9 offset:4096
	ds_read_b32 v197, v9 offset:4608
	ds_read_b32 v198, v9 offset:5120
	ds_read_b32 v199, v9 offset:5632
	ds_read_b32 v200, v9 offset:6144
	ds_read_b32 v201, v9 offset:6656
	ds_read_b32 v202, v9 offset:7168
	ds_read_b32 v203, v9 offset:7680
	s_waitcnt lgkmcnt(0)
	v_max_f32_e32 v170, v170, v170
	v_max_f32_e32 v171, v171, v171
	v_max_f32_e32 v172, v172, v172
	v_max_f32_e32 v173, v173, v173
	v_max_f32_e32 v174, v174, v174
	v_max_f32_e32 v175, v175, v175
	v_max_f32_e32 v176, v176, v176
	v_max_f32_e32 v177, v177, v177
	v_max_f32_e32 v196, v196, v196
	v_max_f32_e32 v197, v197, v197
	v_max_f32_e32 v198, v198, v198
	v_max_f32_e32 v199, v199, v199
	v_max_f32_e32 v200, v200, v200
	v_max_f32_e32 v201, v201, v201
	v_max_f32_e32 v202, v202, v202
	v_max_f32_e32 v203, v203, v203
	v_med3_f32 v170, v170, s20, v13
	v_med3_f32 v171, v171, s20, v13
	v_med3_f32 v172, v172, s20, v13
	v_med3_f32 v173, v173, s20, v13
	v_med3_f32 v174, v174, s20, v13
	v_med3_f32 v175, v175, s20, v13
	v_med3_f32 v176, v176, s20, v13
	v_med3_f32 v177, v177, s20, v13
	v_med3_f32 v196, v196, s20, v13
	v_med3_f32 v197, v197, s20, v13
	v_med3_f32 v198, v198, s20, v13
	v_med3_f32 v199, v199, s20, v13
	v_med3_f32 v200, v200, s20, v13
	v_med3_f32 v201, v201, s20, v13
	v_med3_f32 v202, v202, s20, v13
	v_med3_f32 v203, v203, s20, v13
	v_mov_b32_e32 v208, 0
	v_mov_b32_e32 v209, 0
	v_mov_b32_e32 v210, 0
	v_mov_b32_e32 v211, 0
	v_cvt_pk_fp8_f32 v208, v170, v171
	v_cvt_pk_fp8_f32 v209, v174, v175
	v_cvt_pk_fp8_f32 v210, v196, v197
	v_cvt_pk_fp8_f32 v211, v200, v201
	v_cvt_pk_fp8_f32 v208, v172, v173 op_sel:[0,0,1]
	v_cvt_pk_fp8_f32 v209, v176, v177 op_sel:[0,0,1]
	v_cvt_pk_fp8_f32 v210, v198, v199 op_sel:[0,0,1]
	v_cvt_pk_fp8_f32 v211, v202, v203 op_sel:[0,0,1]
	s_nop 0
	global_store_dwordx4 v12, v[208:211], s[14:15]
	s_waitcnt vmcnt(32)
	v_mul_f32_e32 v100, 0x43000000, v100
	v_mul_f32_e32 v101, 0x43000000, v101
	v_mul_f32_e32 v102, 0x43000000, v102
	v_mul_f32_e32 v103, 0x43000000, v103
	ds_write_b128 v4, v[100:103]
	v_mul_f32_e32 v104, 0x43000000, v104
	v_mul_f32_e32 v105, 0x43000000, v105
	v_mul_f32_e32 v106, 0x43000000, v106
	v_mul_f32_e32 v107, 0x43000000, v107
	ds_write_b128 v4, v[104:107] offset:1024
	v_mul_f32_e32 v108, 0x43000000, v108
	v_mul_f32_e32 v109, 0x43000000, v109
	v_mul_f32_e32 v110, 0x43000000, v110
	v_mul_f32_e32 v111, 0x43000000, v111
	ds_write_b128 v4, v[108:111] offset:2048
	v_mul_f32_e32 v112, 0x43000000, v112
	v_mul_f32_e32 v113, 0x43000000, v113
	v_mul_f32_e32 v114, 0x43000000, v114
	v_mul_f32_e32 v115, 0x43000000, v115
	ds_write_b128 v4, v[112:115] offset:3072
	v_mul_f32_e32 v116, 0x43000000, v116
	v_mul_f32_e32 v117, 0x43000000, v117
	v_mul_f32_e32 v118, 0x43000000, v118
	v_mul_f32_e32 v119, 0x43000000, v119
	ds_write_b128 v4, v[116:119] offset:4096
	v_mul_f32_e32 v120, 0x43000000, v120
	v_mul_f32_e32 v121, 0x43000000, v121
	v_mul_f32_e32 v122, 0x43000000, v122
	v_mul_f32_e32 v123, 0x43000000, v123
	ds_write_b128 v4, v[120:123] offset:5120
	v_mul_f32_e32 v124, 0x43000000, v124
	v_mul_f32_e32 v125, 0x43000000, v125
	v_mul_f32_e32 v126, 0x43000000, v126
	v_mul_f32_e32 v127, 0x43000000, v127
	ds_write_b128 v4, v[124:127] offset:6144
	v_mul_f32_e32 v128, 0x43000000, v128
	v_mul_f32_e32 v129, 0x43000000, v129
	v_mul_f32_e32 v130, 0x43000000, v130
	v_mul_f32_e32 v131, 0x43000000, v131
	ds_write_b128 v4, v[128:131] offset:7168
	s_waitcnt lgkmcnt(0)
	s_barrier
; #define GAS __attribute__((address_space(1)))
; #define LAS __attribute__((address_space(3)))
; #define LDS_WAIT() asm volatile("s_waitcnt lgkmcnt(0)" ::: "memory")
;     const int pr = item >> 1, kb = 2 * (pr / nblk) + (item & 1), nb = pr % nblk, k0 = 64 * kb, n0 = 32 * nb;
;     const int nr = n0 + (lane & 31); const int sc = MAP == 1 ? src_col_in(nr) : nr;
;     float v[32];
; #pragma unroll
;     for (int i = 0; i < 32; ++i) v[i] = sc >= 0 ? W[(size_t)(k0 + 2 * i + (lane >> 5)) * Nsrc + sc] : 0.f;
; #pragma unroll
;     for (int i = 0; i < 32; ++i) { const int k = k0 + 2 * i + (lane >> 5); float x = v[i] * wscale; if (KS) x *= (k < ksplit ? ksA[k] : ksB[k - ksplit]); scr[(2 * i + (lane >> 5)) * 33 + (lane & 31)] = x; }
;     LDS_WAIT(); asm volatile("" ::: "memory");
;     const int c = lane & 7;
; #pragma unroll
;     for (int j = 0; j < 4; ++j) { const int n = (lane >> 3) + 8 * j; const LAS float* s = scr + (8 * c) * 33 + n;
;         const unsigned long long o = (unsigned long long)pg8::pk4_fp8(s[0 * 33], s[1 * 33], s[2 * 33], s[3 * 33]) | ((unsigned long long)pg8::pk4_fp8(s[4 * 33], s[5 * 33], s[6 * 33], s[7 * 33]) << 32);
;         *(GAS unsigned long long*)(WT + (size_t)(n0 + n) * K + k0 + 8 * c) = o; }
;     LDS_WAIT(); asm volatile("" ::: "memory");
; }
; __global__ void __launch_bounds__(NWAVES * 64, 2) hybrid_fwd(Args args) {
;     ...
;             p0_transpose_item_f8<false>(args.in[16] + (size_t)l * FF * DM, FF, DM, DM / 32, (unsigned char*)(ws + WS_WDN + l * SZ_WDN), 128.f, args.in[16], args.in[16], 0, scr, r, lane);
	s_add_i32 s17, s16, 4032
	s_min_u32 s17, s17, 0xfff
	s_lshr_b32 s18, s17, 5
	s_add_i32 s18, s18, 0
	s_and_b32 s19, s17, 31
	s_lshl_b32 s18, s18, 21
	s_lshl_b32 s19, s19, 9
	s_add_u32 s18, s18, s19
	s_add_u32 s12, s2, s18
	s_addc_u32 s13, s3, 0
	global_load_dwordx4 v[100:103], v10, s[12:13]
	s_add_u32 s12, s12, 0x8000
	s_addc_u32 s13, s13, 0
	global_load_dwordx4 v[104:107], v10, s[12:13]
	s_add_u32 s12, s12, 0x8000
	s_addc_u32 s13, s13, 0
	global_load_dwordx4 v[108:111], v10, s[12:13]
	s_add_u32 s12, s12, 0x8000
	s_addc_u32 s13, s13, 0
	global_load_dwordx4 v[112:115], v10, s[12:13]
	s_add_u32 s12, s12, 0x8000
	s_addc_u32 s13, s13, 0
	global_load_dwordx4 v[116:119], v10, s[12:13]
	s_add_u32 s12, s12, 0x8000
	s_addc_u32 s13, s13, 0
	global_load_dwordx4 v[120:123], v10, s[12:13]
	s_add_u32 s12, s12, 0x8000
	s_addc_u32 s13, s13, 0
	global_load_dwordx4 v[124:127], v10, s[12:13]
	s_add_u32 s12, s12, 0x8000
	s_addc_u32 s13, s13, 0
	global_load_dwordx4 v[128:131], v10, s[12:13]
	s_add_i32 s17, s16, 3648
	s_min_u32 s17, s17, 0xfff
	s_lshr_b32 s18, s17, 5
	s_add_i32 s18, s18, 0
	s_and_b32 s19, s17, 31
	s_lshl_b32 s19, s19, 21
	s_lshl_b32 s18, s18, 7
	s_add_u32 s18, s18, s19
	s_add_u32 s14, s4, s18
	s_addc_u32 s15, s5, 0
	ds_read_b32 v170, v6
	ds_read_b32 v171, v6 offset:512
	ds_read_b32 v172, v6 offset:1024
	ds_read_b32 v173, v6 offset:1536
	ds_read_b32 v174, v6 offset:2048
	ds_read_b32 v175, v6 offset:2560
	ds_read_b32 v176, v6 offset:3072
	ds_read_b32 v177, v6 offset:3584
	ds_read_b32 v196, v6 offset:4096
	ds_read_b32 v197, v6 offset:4608
	ds_read_b32 v198, v6 offset:5120
	ds_read_b32 v199, v6 offset:5632
	ds_read_b32 v200, v6 offset:6144
	ds_read_b32 v201, v6 offset:6656
	ds_read_b32 v202, v6 offset:7168
	ds_read_b32 v203, v6 offset:7680
	s_waitcnt lgkmcnt(0)
	v_max_f32_e32 v170, v170, v170
	v_max_f32_e32 v171, v171, v171
	v_max_f32_e32 v172, v172, v172
	v_max_f32_e32 v173, v173, v173
	v_max_f32_e32 v174, v174, v174
	v_max_f32_e32 v175, v175, v175
	v_max_f32_e32 v176, v176, v176
	v_max_f32_e32 v177, v177, v177
	v_max_f32_e32 v196, v196, v196
	v_max_f32_e32 v197, v197, v197
	v_max_f32_e32 v198, v198, v198
	v_max_f32_e32 v199, v199, v199
	v_max_f32_e32 v200, v200, v200
	v_max_f32_e32 v201, v201, v201
	v_max_f32_e32 v202, v202, v202
	v_max_f32_e32 v203, v203, v203
	v_med3_f32 v170, v170, s20, v13
	v_med3_f32 v171, v171, s20, v13
	v_med3_f32 v172, v172, s20, v13
	v_med3_f32 v173, v173, s20, v13
	v_med3_f32 v174, v174, s20, v13
	v_med3_f32 v175, v175, s20, v13
	v_med3_f32 v176, v176, s20, v13
	v_med3_f32 v177, v177, s20, v13
	v_med3_f32 v196, v196, s20, v13
	v_med3_f32 v197, v197, s20, v13
	v_med3_f32 v198, v198, s20, v13
	v_med3_f32 v199, v199, s20, v13
	v_med3_f32 v200, v200, s20, v13
	v_med3_f32 v201, v201, s20, v13
	v_med3_f32 v202, v202, s20, v13
	v_med3_f32 v203, v203, s20, v13
	v_mov_b32_e32 v208, 0
	v_mov_b32_e32 v209, 0
	v_mov_b32_e32 v210, 0
	v_mov_b32_e32 v211, 0
	v_cvt_pk_fp8_f32 v208, v170, v171
	v_cvt_pk_fp8_f32 v209, v174, v175
	v_cvt_pk_fp8_f32 v210, v196, v197
	v_cvt_pk_fp8_f32 v211, v200, v201
	v_cvt_pk_fp8_f32 v208, v172, v173 op_sel:[0,0,1]
	v_cvt_pk_fp8_f32 v209, v176, v177 op_sel:[0,0,1]
	v_cvt_pk_fp8_f32 v210, v198, v199 op_sel:[0,0,1]
	v_cvt_pk_fp8_f32 v211, v202, v203 op_sel:[0,0,1]
	s_nop 0
	global_store_dwordx4 v11, v[208:211], s[14:15]
	ds_read_b32 v170, v8
	ds_read_b32 v171, v8 offset:512
	ds_read_b32 v172, v8 offset:1024
	ds_read_b32 v173, v8 offset:1536
	ds_read_b32 v174, v8 offset:2048
	ds_read_b32 v175, v8 offset:2560
	ds_read_b32 v176, v8 offset:3072
	ds_read_b32 v177, v8 offset:3584
	ds_read_b32 v196, v8 offset:4096
	ds_read_b32 v197, v8 offset:4608
	ds_read_b32 v198, v8 offset:5120
	ds_read_b32 v199, v8 offset:5632
	ds_read_b32 v200, v8 offset:6144
	ds_read_b32 v201, v8 offset:6656
	ds_read_b32 v202, v8 offset:7168
	ds_read_b32 v203, v8 offset:7680
	s_waitcnt lgkmcnt(0)
	v_max_f32_e32 v170, v170, v170
	v_max_f32_e32 v171, v171, v171
	v_max_f32_e32 v172, v172, v172
	v_max_f32_e32 v173, v173, v173
	v_max_f32_e32 v174, v174, v174
	v_max_f32_e32 v175, v175, v175
	v_max_f32_e32 v176, v176, v176
	v_max_f32_e32 v177, v177, v177
	v_max_f32_e32 v196, v196, v196
	v_max_f32_e32 v197, v197, v197
	v_max_f32_e32 v198, v198, v198
	v_max_f32_e32 v199, v199, v199
	v_max_f32_e32 v200, v200, v200
	v_max_f32_e32 v201, v201, v201
	v_max_f32_e32 v202, v202, v202
	v_max_f32_e32 v203, v203, v203
	v_med3_f32 v170, v170, s20, v13
	v_med3_f32 v171, v171, s20, v13
	v_med3_f32 v172, v172, s20, v13
	v_med3_f32 v173, v173, s20, v13
	v_med3_f32 v174, v174, s20, v13
	v_med3_f32 v175, v175, s20, v13
	v_med3_f32 v176, v176, s20, v13
	v_med3_f32 v177, v177, s20, v13
	v_med3_f32 v196, v196, s20, v13
	v_med3_f32 v197, v197, s20, v13
	v_med3_f32 v198, v198, s20, v13
	v_med3_f32 v199, v199, s20, v13
	v_med3_f32 v200, v200, s20, v13
	v_med3_f32 v201, v201, s20, v13
	v_med3_f32 v202, v202, s20, v13
	v_med3_f32 v203, v203, s20, v13
	v_mov_b32_e32 v208, 0
	v_mov_b32_e32 v209, 0
	v_mov_b32_e32 v210, 0
	v_mov_b32_e32 v211, 0
	v_cvt_pk_fp8_f32 v208, v170, v171
	v_cvt_pk_fp8_f32 v209, v174, v175
	v_cvt_pk_fp8_f32 v210, v196, v197
	v_cvt_pk_fp8_f32 v211, v200, v201
	v_cvt_pk_fp8_f32 v208, v172, v173 op_sel:[0,0,1]
	v_cvt_pk_fp8_f32 v209, v176, v177 op_sel:[0,0,1]
	v_cvt_pk_fp8_f32 v210, v198, v199 op_sel:[0,0,1]
	v_cvt_pk_fp8_f32 v211, v202, v203 op_sel:[0,0,1]
	s_nop 0
	global_store_dwordx4 v12, v[208:211], s[14:15]
	s_waitcnt vmcnt(32)
	v_mul_f32_e32 v132, 0x43000000, v132
	v_mul_f32_e32 v133, 0x43000000, v133
	v_mul_f32_e32 v134, 0x43000000, v134
	v_mul_f32_e32 v135, 0x43000000, v135
	ds_write_b128 v5, v[132:135]
	v_mul_f32_e32 v136, 0x43000000, v136
	v_mul_f32_e32 v137, 0x43000000, v137
	v_mul_f32_e32 v138, 0x43000000, v138
	v_mul_f32_e32 v139, 0x43000000, v139
	ds_write_b128 v5, v[136:139] offset:1024
	v_mul_f32_e32 v140, 0x43000000, v140
	v_mul_f32_e32 v141, 0x43000000, v141
	v_mul_f32_e32 v142, 0x43000000, v142
	v_mul_f32_e32 v143, 0x43000000, v143
	ds_write_b128 v5, v[140:143] offset:2048
	v_mul_f32_e32 v144, 0x43000000, v144
	v_mul_f32_e32 v145, 0x43000000, v145
	v_mul_f32_e32 v146, 0x43000000, v146
	v_mul_f32_e32 v147, 0x43000000, v147
	ds_write_b128 v5, v[144:147] offset:3072
	v_mul_f32_e32 v148, 0x43000000, v148
	v_mul_f32_e32 v149, 0x43000000, v149
	v_mul_f32_e32 v150, 0x43000000, v150
	v_mul_f32_e32 v151, 0x43000000, v151
	ds_write_b128 v5, v[148:151] offset:4096
	v_mul_f32_e32 v152, 0x43000000, v152
	v_mul_f32_e32 v153, 0x43000000, v153
	v_mul_f32_e32 v154, 0x43000000, v154
	v_mul_f32_e32 v155, 0x43000000, v155
	ds_write_b128 v5, v[152:155] offset:5120
	v_mul_f32_e32 v156, 0x43000000, v156
	v_mul_f32_e32 v157, 0x43000000, v157
	v_mul_f32_e32 v158, 0x43000000, v158
	v_mul_f32_e32 v159, 0x43000000, v159
	ds_write_b128 v5, v[156:159] offset:6144
	v_mul_f32_e32 v160, 0x43000000, v160
	v_mul_f32_e32 v161, 0x43000000, v161
	v_mul_f32_e32 v162, 0x43000000, v162
	v_mul_f32_e32 v163, 0x43000000, v163
	ds_write_b128 v5, v[160:163] offset:7168
	s_waitcnt lgkmcnt(0)
	s_barrier
; #define GAS __attribute__((address_space(1)))
; #define LAS __attribute__((address_space(3)))
; #define LDS_WAIT() asm volatile("s_waitcnt lgkmcnt(0)" ::: "memory")
;     const int pr = item >> 1, kb = 2 * (pr / nblk) + (item & 1), nb = pr % nblk, k0 = 64 * kb, n0 = 32 * nb;
;     const int nr = n0 + (lane & 31); const int sc = MAP == 1 ? src_col_in(nr) : nr;
;     float v[32];
; #pragma unroll
;     for (int i = 0; i < 32; ++i) v[i] = sc >= 0 ? W[(size_t)(k0 + 2 * i + (lane >> 5)) * Nsrc + sc] : 0.f;
; #pragma unroll
;     for (int i = 0; i < 32; ++i) { const int k = k0 + 2 * i + (lane >> 5); float x = v[i] * wscale; if (KS) x *= (k < ksplit ? ksA[k] : ksB[k - ksplit]); scr[(2 * i + (lane >> 5)) * 33 + (lane & 31)] = x; }
;     LDS_WAIT(); asm volatile("" ::: "memory");
;     const int c = lane & 7;
; #pragma unroll
;     for (int j = 0; j < 4; ++j) { const int n = (lane >> 3) + 8 * j; const LAS float* s = scr + (8 * c) * 33 + n;
;         const unsigned long long o = (unsigned long long)pg8::pk4_fp8(s[0 * 33], s[1 * 33], s[2 * 33], s[3 * 33]) | ((unsigned long long)pg8::pk4_fp8(s[4 * 33], s[5 * 33], s[6 * 33], s[7 * 33]) << 32);
;         *(GAS unsigned long long*)(WT + (size_t)(n0 + n) * K + k0 + 8 * c) = o; }
;     LDS_WAIT(); asm volatile("" ::: "memory");
; }
; __global__ void __launch_bounds__(NWAVES * 64, 2) hybrid_fwd(Args args) {
;     ...
;             if (r < I_O) { if (l >= WO_F8_FROM) p0_transpose_item_f8<true>(args.in[13] + (size_t)l * DM * DM, DM, DM, DM / 32, (unsigned char*)(ws + WS_WO + l * SZ_WO), 64.f, args.in[6] + l * 2048, args.in[12] + l * 2048, 2048, scr, r, lane);
	s_add_i32 s19, s39, 0
	s_min_u32 s19, s19, 31
	s_lshl_b32 s19, s19, 9
	s_add_u32 s12, s22, s19
	s_addc_u32 s13, s23, 0
	global_load_dwordx4 v[132:135], v10, s[12:13]
	s_add_u32 s12, s12, 0x8000
	s_addc_u32 s13, s13, 0
	global_load_dwordx4 v[136:139], v10, s[12:13]
	s_add_u32 s12, s12, 0x8000
	s_addc_u32 s13, s13, 0
	global_load_dwordx4 v[140:143], v10, s[12:13]
	s_add_u32 s12, s12, 0x8000
	s_addc_u32 s13, s13, 0
	global_load_dwordx4 v[144:147], v10, s[12:13]
	s_add_u32 s12, s12, 0x8000
	s_addc_u32 s13, s13, 0
	global_load_dwordx4 v[148:151], v10, s[12:13]
	s_add_u32 s12, s12, 0x8000
	s_addc_u32 s13, s13, 0
	global_load_dwordx4 v[152:155], v10, s[12:13]
	s_add_u32 s12, s12, 0x8000
	s_addc_u32 s13, s13, 0
	global_load_dwordx4 v[156:159], v10, s[12:13]
	s_add_u32 s12, s12, 0x8000
	s_addc_u32 s13, s13, 0
	global_load_dwordx4 v[160:163], v10, s[12:13]
	s_add_i32 s17, s16, 3744
	s_min_u32 s17, s17, 0xfff
	s_lshr_b32 s18, s17, 5
	s_add_i32 s18, s18, 0
	s_and_b32 s19, s17, 31
	s_lshl_b32 s19, s19, 21
	s_lshl_b32 s18, s18, 7
	s_add_u32 s18, s18, s19
	s_add_u32 s14, s4, s18
	s_addc_u32 s15, s5, 0
	ds_read_b32 v170, v7
	ds_read_b32 v171, v7 offset:512
	ds_read_b32 v172, v7 offset:1024
	ds_read_b32 v173, v7 offset:1536
	ds_read_b32 v174, v7 offset:2048
	ds_read_b32 v175, v7 offset:2560
	ds_read_b32 v176, v7 offset:3072
	ds_read_b32 v177, v7 offset:3584
	ds_read_b32 v196, v7 offset:4096
	ds_read_b32 v197, v7 offset:4608
	ds_read_b32 v198, v7 offset:5120
	ds_read_b32 v199, v7 offset:5632
	ds_read_b32 v200, v7 offset:6144
	ds_read_b32 v201, v7 offset:6656
	ds_read_b32 v202, v7 offset:7168
	ds_read_b32 v203, v7 offset:7680
	s_waitcnt lgkmcnt(0)
	v_max_f32_e32 v170, v170, v170
	v_max_f32_e32 v171, v171, v171
	v_max_f32_e32 v172, v172, v172
	v_max_f32_e32 v173, v173, v173
	v_max_f32_e32 v174, v174, v174
	v_max_f32_e32 v175, v175, v175
	v_max_f32_e32 v176, v176, v176
	v_max_f32_e32 v177, v177, v177
	v_max_f32_e32 v196, v196, v196
	v_max_f32_e32 v197, v197, v197
	v_max_f32_e32 v198, v198, v198
	v_max_f32_e32 v199, v199, v199
	v_max_f32_e32 v200, v200, v200
	v_max_f32_e32 v201, v201, v201
	v_max_f32_e32 v202, v202, v202
	v_max_f32_e32 v203, v203, v203
	v_med3_f32 v170, v170, s20, v13
	v_med3_f32 v171, v171, s20, v13
	v_med3_f32 v172, v172, s20, v13
	v_med3_f32 v173, v173, s20, v13
	v_med3_f32 v174, v174, s20, v13
	v_med3_f32 v175, v175, s20, v13
	v_med3_f32 v176, v176, s20, v13
	v_med3_f32 v177, v177, s20, v13
	v_med3_f32 v196, v196, s20, v13
	v_med3_f32 v197, v197, s20, v13
	v_med3_f32 v198, v198, s20, v13
	v_med3_f32 v199, v199, s20, v13
	v_med3_f32 v200, v200, s20, v13
	v_med3_f32 v201, v201, s20, v13
	v_med3_f32 v202, v202, s20, v13
	v_med3_f32 v203, v203, s20, v13
	v_mov_b32_e32 v208, 0
	v_mov_b32_e32 v209, 0
	v_mov_b32_e32 v210, 0
	v_mov_b32_e32 v211, 0
	v_cvt_pk_fp8_f32 v208, v170, v171
	v_cvt_pk_fp8_f32 v209, v174, v175
	v_cvt_pk_fp8_f32 v210, v196, v197
	v_cvt_pk_fp8_f32 v211, v200, v201
	v_cvt_pk_fp8_f32 v208, v172, v173 op_sel:[0,0,1]
	v_cvt_pk_fp8_f32 v209, v176, v177 op_sel:[0,0,1]
	v_cvt_pk_fp8_f32 v210, v198, v199 op_sel:[0,0,1]
	v_cvt_pk_fp8_f32 v211, v202, v203 op_sel:[0,0,1]
	s_nop 0
	global_store_dwordx4 v11, v[208:211], s[14:15]
	ds_read_b32 v170, v9
	ds_read_b32 v171, v9 offset:512
	ds_read_b32 v172, v9 offset:1024
	ds_read_b32 v173, v9 offset:1536
	ds_read_b32 v174, v9 offset:2048
	ds_read_b32 v175, v9 offset:2560
	ds_read_b32 v176, v9 offset:3072
	ds_read_b32 v177, v9 offset:3584
	ds_read_b32 v196, v9 offset:4096
	ds_read_b32 v197, v9 offset:4608
	ds_read_b32 v198, v9 offset:5120
	ds_read_b32 v199, v9 offset:5632
	ds_read_b32 v200, v9 offset:6144
	ds_read_b32 v201, v9 offset:6656
	ds_read_b32 v202, v9 offset:7168
	ds_read_b32 v203, v9 offset:7680
	s_waitcnt lgkmcnt(0)
	v_max_f32_e32 v170, v170, v170
	v_max_f32_e32 v171, v171, v171
	v_max_f32_e32 v172, v172, v172
	v_max_f32_e32 v173, v173, v173
	v_max_f32_e32 v174, v174, v174
	v_max_f32_e32 v175, v175, v175
	v_max_f32_e32 v176, v176, v176
	v_max_f32_e32 v177, v177, v177
	v_max_f32_e32 v196, v196, v196
	v_max_f32_e32 v197, v197, v197
	v_max_f32_e32 v198, v198, v198
	v_max_f32_e32 v199, v199, v199
	v_max_f32_e32 v200, v200, v200
	v_max_f32_e32 v201, v201, v201
	v_max_f32_e32 v202, v202, v202
	v_max_f32_e32 v203, v203, v203
	v_med3_f32 v170, v170, s20, v13
	v_med3_f32 v171, v171, s20, v13
	v_med3_f32 v172, v172, s20, v13
	v_med3_f32 v173, v173, s20, v13
	v_med3_f32 v174, v174, s20, v13
	v_med3_f32 v175, v175, s20, v13
	v_med3_f32 v176, v176, s20, v13
	v_med3_f32 v177, v177, s20, v13
	v_med3_f32 v196, v196, s20, v13
	v_med3_f32 v197, v197, s20, v13
	v_med3_f32 v198, v198, s20, v13
	v_med3_f32 v199, v199, s20, v13
	v_med3_f32 v200, v200, s20, v13
	v_med3_f32 v201, v201, s20, v13
	v_med3_f32 v202, v202, s20, v13
	v_med3_f32 v203, v203, s20, v13
	v_mov_b32_e32 v208, 0
	v_mov_b32_e32 v209, 0
	v_mov_b32_e32 v210, 0
	v_mov_b32_e32 v211, 0
	v_cvt_pk_fp8_f32 v208, v170, v171
	v_cvt_pk_fp8_f32 v209, v174, v175
	v_cvt_pk_fp8_f32 v210, v196, v197
	v_cvt_pk_fp8_f32 v211, v200, v201
	v_cvt_pk_fp8_f32 v208, v172, v173 op_sel:[0,0,1]
	v_cvt_pk_fp8_f32 v209, v176, v177 op_sel:[0,0,1]
	v_cvt_pk_fp8_f32 v210, v198, v199 op_sel:[0,0,1]
	v_cvt_pk_fp8_f32 v211, v202, v203 op_sel:[0,0,1]
	s_nop 0
	global_store_dwordx4 v12, v[208:211], s[14:15]
	s_waitcnt vmcnt(32)
	v_mul_f32_e32 v36, 0x43000000, v36
	v_mul_f32_e32 v37, 0x43000000, v37
	v_mul_f32_e32 v38, 0x43000000, v38
	v_mul_f32_e32 v39, 0x43000000, v39
	ds_write_b128 v4, v[36:39]
	v_mul_f32_e32 v40, 0x43000000, v40
	v_mul_f32_e32 v41, 0x43000000, v41
	v_mul_f32_e32 v42, 0x43000000, v42
	v_mul_f32_e32 v43, 0x43000000, v43
	ds_write_b128 v4, v[40:43] offset:1024
	v_mul_f32_e32 v44, 0x43000000, v44
	v_mul_f32_e32 v45, 0x43000000, v45
	v_mul_f32_e32 v46, 0x43000000, v46
	v_mul_f32_e32 v47, 0x43000000, v47
	ds_write_b128 v4, v[44:47] offset:2048
	v_mul_f32_e32 v48, 0x43000000, v48
	v_mul_f32_e32 v49, 0x43000000, v49
	v_mul_f32_e32 v50, 0x43000000, v50
	v_mul_f32_e32 v51, 0x43000000, v51
	ds_write_b128 v4, v[48:51] offset:3072
	v_mul_f32_e32 v52, 0x43000000, v52
	v_mul_f32_e32 v53, 0x43000000, v53
	v_mul_f32_e32 v54, 0x43000000, v54
	v_mul_f32_e32 v55, 0x43000000, v55
	ds_write_b128 v4, v[52:55] offset:4096
	v_mul_f32_e32 v56, 0x43000000, v56
	v_mul_f32_e32 v57, 0x43000000, v57
	v_mul_f32_e32 v58, 0x43000000, v58
	v_mul_f32_e32 v59, 0x43000000, v59
	ds_write_b128 v4, v[56:59] offset:5120
	v_mul_f32_e32 v60, 0x43000000, v60
	v_mul_f32_e32 v61, 0x43000000, v61
	v_mul_f32_e32 v62, 0x43000000, v62
	v_mul_f32_e32 v63, 0x43000000, v63
	ds_write_b128 v4, v[60:63] offset:6144
	v_mul_f32_e32 v64, 0x43000000, v64
	v_mul_f32_e32 v65, 0x43000000, v65
	v_mul_f32_e32 v66, 0x43000000, v66
	v_mul_f32_e32 v67, 0x43000000, v67
	ds_write_b128 v4, v[64:67] offset:7168
	s_waitcnt lgkmcnt(0)
	s_barrier
; #define GAS __attribute__((address_space(1)))
; #define LAS __attribute__((address_space(3)))
; #define LDS_WAIT() asm volatile("s_waitcnt lgkmcnt(0)" ::: "memory")
;     const int pr = item >> 1, kb = 2 * (pr / nblk) + (item & 1), nb = pr % nblk, k0 = 64 * kb, n0 = 32 * nb;
;     const int nr = n0 + (lane & 31); const int sc = MAP == 1 ? src_col_in(nr) : nr;
;     float v[32];
; #pragma unroll
;     for (int i = 0; i < 32; ++i) v[i] = sc >= 0 ? W[(size_t)(k0 + 2 * i + (lane >> 5)) * Nsrc + sc] : 0.f;
; #pragma unroll
;     for (int i = 0; i < 32; ++i) { const int k = k0 + 2 * i + (lane >> 5); float x = v[i] * wscale; if (KS) x *= (k < ksplit ? ksA[k] : ksB[k - ksplit]); scr[(2 * i + (lane >> 5)) * 33 + (lane & 31)] = x; }
;     LDS_WAIT(); asm volatile("" ::: "memory");
;     const int c = lane & 7;
; #pragma unroll
;     for (int j = 0; j < 4; ++j) { const int n = (lane >> 3) + 8 * j; const LAS float* s = scr + (8 * c) * 33 + n;
;         const unsigned long long o = (unsigned long long)pg8::pk4_fp8(s[0 * 33], s[1 * 33], s[2 * 33], s[3 * 33]) | ((unsigned long long)pg8::pk4_fp8(s[4 * 33], s[5 * 33], s[6 * 33], s[7 * 33]) << 32);
;         *(GAS unsigned long long*)(WT + (size_t)(n0 + n) * K + k0 + 8 * c) = o; }
;     LDS_WAIT(); asm volatile("" ::: "memory");
; }
; __global__ void __launch_bounds__(NWAVES * 64, 2) hybrid_fwd(Args args) {
;     ...
;             if (r < I_O) { if (l >= WO_F8_FROM) p0_transpose_item_f8<true>(args.in[13] + (size_t)l * DM * DM, DM, DM, DM / 32, (unsigned char*)(ws + WS_WO + l * SZ_WO), 64.f, args.in[6] + l * 2048, args.in[12] + l * 2048, 2048, scr, r, lane);
	s_add_i32 s19, s39, 3
	s_min_u32 s19, s19, 31
	s_lshl_b32 s19, s19, 9
	s_add_u32 s12, s22, s19
	s_addc_u32 s13, s23, 0
	global_load_dwordx4 v[36:39], v10, s[12:13]
	s_add_u32 s12, s12, 0x8000
	s_addc_u32 s13, s13, 0
	global_load_dwordx4 v[40:43], v10, s[12:13]
	s_add_u32 s12, s12, 0x8000
	s_addc_u32 s13, s13, 0
	global_load_dwordx4 v[44:47], v10, s[12:13]
	s_add_u32 s12, s12, 0x8000
	s_addc_u32 s13, s13, 0
	global_load_dwordx4 v[48:51], v10, s[12:13]
	s_add_u32 s12, s12, 0x8000
	s_addc_u32 s13, s13, 0
	global_load_dwordx4 v[52:55], v10, s[12:13]
	s_add_u32 s12, s12, 0x8000
	s_addc_u32 s13, s13, 0
	global_load_dwordx4 v[56:59], v10, s[12:13]
	s_add_u32 s12, s12, 0x8000
	s_addc_u32 s13, s13, 0
	global_load_dwordx4 v[60:63], v10, s[12:13]
	s_add_u32 s12, s12, 0x8000
	s_addc_u32 s13, s13, 0
	global_load_dwordx4 v[64:67], v10, s[12:13]
	s_add_i32 s17, s16, 3840
	s_min_u32 s17, s17, 0xfff
	s_lshr_b32 s18, s17, 5
	s_add_i32 s18, s18, 0
	s_and_b32 s19, s17, 31
	s_lshl_b32 s19, s19, 21
	s_lshl_b32 s18, s18, 7
	s_add_u32 s18, s18, s19
	s_add_u32 s14, s4, s18
	s_addc_u32 s15, s5, 0
	ds_read_b32 v170, v6
	ds_read_b32 v171, v6 offset:512
	ds_read_b32 v172, v6 offset:1024
	ds_read_b32 v173, v6 offset:1536
	ds_read_b32 v174, v6 offset:2048
	ds_read_b32 v175, v6 offset:2560
	ds_read_b32 v176, v6 offset:3072
	ds_read_b32 v177, v6 offset:3584
	ds_read_b32 v196, v6 offset:4096
	ds_read_b32 v197, v6 offset:4608
	ds_read_b32 v198, v6 offset:5120
	ds_read_b32 v199, v6 offset:5632
	ds_read_b32 v200, v6 offset:6144
	ds_read_b32 v201, v6 offset:6656
	ds_read_b32 v202, v6 offset:7168
	ds_read_b32 v203, v6 offset:7680
	s_waitcnt lgkmcnt(0)
	v_max_f32_e32 v170, v170, v170
	v_max_f32_e32 v171, v171, v171
	v_max_f32_e32 v172, v172, v172
	v_max_f32_e32 v173, v173, v173
	v_max_f32_e32 v174, v174, v174
	v_max_f32_e32 v175, v175, v175
	v_max_f32_e32 v176, v176, v176
	v_max_f32_e32 v177, v177, v177
	v_max_f32_e32 v196, v196, v196
	v_max_f32_e32 v197, v197, v197
	v_max_f32_e32 v198, v198, v198
	v_max_f32_e32 v199, v199, v199
	v_max_f32_e32 v200, v200, v200
	v_max_f32_e32 v201, v201, v201
	v_max_f32_e32 v202, v202, v202
	v_max_f32_e32 v203, v203, v203
	v_med3_f32 v170, v170, s20, v13
	v_med3_f32 v171, v171, s20, v13
	v_med3_f32 v172, v172, s20, v13
	v_med3_f32 v173, v173, s20, v13
	v_med3_f32 v174, v174, s20, v13
	v_med3_f32 v175, v175, s20, v13
	v_med3_f32 v176, v176, s20, v13
	v_med3_f32 v177, v177, s20, v13
	v_med3_f32 v196, v196, s20, v13
	v_med3_f32 v197, v197, s20, v13
	v_med3_f32 v198, v198, s20, v13
	v_med3_f32 v199, v199, s20, v13
	v_med3_f32 v200, v200, s20, v13
	v_med3_f32 v201, v201, s20, v13
	v_med3_f32 v202, v202, s20, v13
	v_med3_f32 v203, v203, s20, v13
	v_mov_b32_e32 v208, 0
	v_mov_b32_e32 v209, 0
	v_mov_b32_e32 v210, 0
	v_mov_b32_e32 v211, 0
	v_cvt_pk_fp8_f32 v208, v170, v171
	v_cvt_pk_fp8_f32 v209, v174, v175
	v_cvt_pk_fp8_f32 v210, v196, v197
	v_cvt_pk_fp8_f32 v211, v200, v201
	v_cvt_pk_fp8_f32 v208, v172, v173 op_sel:[0,0,1]
	v_cvt_pk_fp8_f32 v209, v176, v177 op_sel:[0,0,1]
	v_cvt_pk_fp8_f32 v210, v198, v199 op_sel:[0,0,1]
	v_cvt_pk_fp8_f32 v211, v202, v203 op_sel:[0,0,1]
	s_nop 0
	global_store_dwordx4 v11, v[208:211], s[14:15]
	ds_read_b32 v170, v8
	ds_read_b32 v171, v8 offset:512
	ds_read_b32 v172, v8 offset:1024
	ds_read_b32 v173, v8 offset:1536
	ds_read_b32 v174, v8 offset:2048
	ds_read_b32 v175, v8 offset:2560
	ds_read_b32 v176, v8 offset:3072
	ds_read_b32 v177, v8 offset:3584
	ds_read_b32 v196, v8 offset:4096
	ds_read_b32 v197, v8 offset:4608
	ds_read_b32 v198, v8 offset:5120
	ds_read_b32 v199, v8 offset:5632
	ds_read_b32 v200, v8 offset:6144
	ds_read_b32 v201, v8 offset:6656
	ds_read_b32 v202, v8 offset:7168
	ds_read_b32 v203, v8 offset:7680
	s_waitcnt lgkmcnt(0)
	v_max_f32_e32 v170, v170, v170
	v_max_f32_e32 v171, v171, v171
	v_max_f32_e32 v172, v172, v172
	v_max_f32_e32 v173, v173, v173
	v_max_f32_e32 v174, v174, v174
	v_max_f32_e32 v175, v175, v175
	v_max_f32_e32 v176, v176, v176
	v_max_f32_e32 v177, v177, v177
	v_max_f32_e32 v196, v196, v196
	v_max_f32_e32 v197, v197, v197
	v_max_f32_e32 v198, v198, v198
	v_max_f32_e32 v199, v199, v199
	v_max_f32_e32 v200, v200, v200
	v_max_f32_e32 v201, v201, v201
	v_max_f32_e32 v202, v202, v202
	v_max_f32_e32 v203, v203, v203
	v_med3_f32 v170, v170, s20, v13
	v_med3_f32 v171, v171, s20, v13
	v_med3_f32 v172, v172, s20, v13
	v_med3_f32 v173, v173, s20, v13
	v_med3_f32 v174, v174, s20, v13
	v_med3_f32 v175, v175, s20, v13
	v_med3_f32 v176, v176, s20, v13
	v_med3_f32 v177, v177, s20, v13
	v_med3_f32 v196, v196, s20, v13
	v_med3_f32 v197, v197, s20, v13
	v_med3_f32 v198, v198, s20, v13
	v_med3_f32 v199, v199, s20, v13
	v_med3_f32 v200, v200, s20, v13
	v_med3_f32 v201, v201, s20, v13
	v_med3_f32 v202, v202, s20, v13
	v_med3_f32 v203, v203, s20, v13
	v_mov_b32_e32 v208, 0
	v_mov_b32_e32 v209, 0
	v_mov_b32_e32 v210, 0
	v_mov_b32_e32 v211, 0
	v_cvt_pk_fp8_f32 v208, v170, v171
	v_cvt_pk_fp8_f32 v209, v174, v175
	v_cvt_pk_fp8_f32 v210, v196, v197
	v_cvt_pk_fp8_f32 v211, v200, v201
	v_cvt_pk_fp8_f32 v208, v172, v173 op_sel:[0,0,1]
	v_cvt_pk_fp8_f32 v209, v176, v177 op_sel:[0,0,1]
	v_cvt_pk_fp8_f32 v210, v198, v199 op_sel:[0,0,1]
	v_cvt_pk_fp8_f32 v211, v202, v203 op_sel:[0,0,1]
	s_nop 0
	global_store_dwordx4 v12, v[208:211], s[14:15]
	s_waitcnt vmcnt(32)
	v_mul_f32_e32 v68, 0x43000000, v68
	v_mul_f32_e32 v69, 0x43000000, v69
	v_mul_f32_e32 v70, 0x43000000, v70
	v_mul_f32_e32 v71, 0x43000000, v71
	ds_write_b128 v5, v[68:71]
	v_mul_f32_e32 v72, 0x43000000, v72
	v_mul_f32_e32 v73, 0x43000000, v73
	v_mul_f32_e32 v74, 0x43000000, v74
	v_mul_f32_e32 v75, 0x43000000, v75
	ds_write_b128 v5, v[72:75] offset:1024
	v_mul_f32_e32 v76, 0x43000000, v76
	v_mul_f32_e32 v77, 0x43000000, v77
	v_mul_f32_e32 v78, 0x43000000, v78
	v_mul_f32_e32 v79, 0x43000000, v79
	ds_write_b128 v5, v[76:79] offset:2048
	v_mul_f32_e32 v80, 0x43000000, v80
	v_mul_f32_e32 v81, 0x43000000, v81
	v_mul_f32_e32 v82, 0x43000000, v82
	v_mul_f32_e32 v83, 0x43000000, v83
	ds_write_b128 v5, v[80:83] offset:3072
	v_mul_f32_e32 v84, 0x43000000, v84
	v_mul_f32_e32 v85, 0x43000000, v85
	v_mul_f32_e32 v86, 0x43000000, v86
	v_mul_f32_e32 v87, 0x43000000, v87
	ds_write_b128 v5, v[84:87] offset:4096
	v_mul_f32_e32 v88, 0x43000000, v88
	v_mul_f32_e32 v89, 0x43000000, v89
	v_mul_f32_e32 v90, 0x43000000, v90
	v_mul_f32_e32 v91, 0x43000000, v91
	ds_write_b128 v5, v[88:91] offset:5120
	v_mul_f32_e32 v92, 0x43000000, v92
	v_mul_f32_e32 v93, 0x43000000, v93
	v_mul_f32_e32 v94, 0x43000000, v94
	v_mul_f32_e32 v95, 0x43000000, v95
	ds_write_b128 v5, v[92:95] offset:6144
	v_mul_f32_e32 v96, 0x43000000, v96
	v_mul_f32_e32 v97, 0x43000000, v97
	v_mul_f32_e32 v98, 0x43000000, v98
	v_mul_f32_e32 v99, 0x43000000, v99
	ds_write_b128 v5, v[96:99] offset:7168
	s_waitcnt lgkmcnt(0)
	s_barrier
; #define GAS __attribute__((address_space(1)))
; #define LAS __attribute__((address_space(3)))
; #define LDS_WAIT() asm volatile("s_waitcnt lgkmcnt(0)" ::: "memory")
;     const int pr = item >> 1, kb = 2 * (pr / nblk) + (item & 1), nb = pr % nblk, k0 = 64 * kb, n0 = 32 * nb;
;     const int nr = n0 + (lane & 31); const int sc = MAP == 1 ? src_col_in(nr) : nr;
;     float v[32];
; #pragma unroll
;     for (int i = 0; i < 32; ++i) v[i] = sc >= 0 ? W[(size_t)(k0 + 2 * i + (lane >> 5)) * Nsrc + sc] : 0.f;
; #pragma unroll
;     for (int i = 0; i < 32; ++i) { const int k = k0 + 2 * i + (lane >> 5); float x = v[i] * wscale; if (KS) x *= (k < ksplit ? ksA[k] : ksB[k - ksplit]); scr[(2 * i + (lane >> 5)) * 33 + (lane & 31)] = x; }
;     LDS_WAIT(); asm volatile("" ::: "memory");
;     const int c = lane & 7;
; #pragma unroll
;     for (int j = 0; j < 4; ++j) { const int n = (lane >> 3) + 8 * j; const LAS float* s = scr + (8 * c) * 33 + n;
;         const unsigned long long o = (unsigned long long)pg8::pk4_fp8(s[0 * 33], s[1 * 33], s[2 * 33], s[3 * 33]) | ((unsigned long long)pg8::pk4_fp8(s[4 * 33], s[5 * 33], s[6 * 33], s[7 * 33]) << 32);
;         *(GAS unsigned long long*)(WT + (size_t)(n0 + n) * K + k0 + 8 * c) = o; }
;     LDS_WAIT(); asm volatile("" ::: "memory");
; }
; __global__ void __launch_bounds__(NWAVES * 64, 2) hybrid_fwd(Args args) {
;     ...
;             if (r < I_O) { if (l >= WO_F8_FROM) p0_transpose_item_f8<true>(args.in[13] + (size_t)l * DM * DM, DM, DM, DM / 32, (unsigned char*)(ws + WS_WO + l * SZ_WO), 64.f, args.in[6] + l * 2048, args.in[12] + l * 2048, 2048, scr, r, lane);
	s_add_i32 s19, s39, 6
	s_min_u32 s19, s19, 31
	s_lshl_b32 s19, s19, 9
	s_add_u32 s12, s22, s19
	s_addc_u32 s13, s23, 0
	global_load_dwordx4 v[68:71], v10, s[12:13]
	s_add_u32 s12, s12, 0x8000
	s_addc_u32 s13, s13, 0
	global_load_dwordx4 v[72:75], v10, s[12:13]
	s_add_u32 s12, s12, 0x8000
	s_addc_u32 s13, s13, 0
	global_load_dwordx4 v[76:79], v10, s[12:13]
	s_add_u32 s12, s12, 0x8000
	s_addc_u32 s13, s13, 0
	global_load_dwordx4 v[80:83], v10, s[12:13]
	s_add_u32 s12, s12, 0x8000
	s_addc_u32 s13, s13, 0
	global_load_dwordx4 v[84:87], v10, s[12:13]
	s_add_u32 s12, s12, 0x8000
	s_addc_u32 s13, s13, 0
	global_load_dwordx4 v[88:91], v10, s[12:13]
	s_add_u32 s12, s12, 0x8000
	s_addc_u32 s13, s13, 0
	global_load_dwordx4 v[92:95], v10, s[12:13]
	s_add_u32 s12, s12, 0x8000
	s_addc_u32 s13, s13, 0
	global_load_dwordx4 v[96:99], v10, s[12:13]
	s_add_i32 s17, s16, 3936
	s_min_u32 s17, s17, 0xfff
	s_lshr_b32 s18, s17, 5
	s_add_i32 s18, s18, 0
	s_and_b32 s19, s17, 31
	s_lshl_b32 s19, s19, 21
	s_lshl_b32 s18, s18, 7
	s_add_u32 s18, s18, s19
	s_add_u32 s14, s4, s18
	s_addc_u32 s15, s5, 0
	ds_read_b32 v170, v7
	ds_read_b32 v171, v7 offset:512
	ds_read_b32 v172, v7 offset:1024
	ds_read_b32 v173, v7 offset:1536
	ds_read_b32 v174, v7 offset:2048
	ds_read_b32 v175, v7 offset:2560
	ds_read_b32 v176, v7 offset:3072
	ds_read_b32 v177, v7 offset:3584
	ds_read_b32 v196, v7 offset:4096
	ds_read_b32 v197, v7 offset:4608
	ds_read_b32 v198, v7 offset:5120
	ds_read_b32 v199, v7 offset:5632
	ds_read_b32 v200, v7 offset:6144
	ds_read_b32 v201, v7 offset:6656
	ds_read_b32 v202, v7 offset:7168
	ds_read_b32 v203, v7 offset:7680
	s_waitcnt lgkmcnt(0)
	v_max_f32_e32 v170, v170, v170
	v_max_f32_e32 v171, v171, v171
	v_max_f32_e32 v172, v172, v172
	v_max_f32_e32 v173, v173, v173
	v_max_f32_e32 v174, v174, v174
	v_max_f32_e32 v175, v175, v175
	v_max_f32_e32 v176, v176, v176
	v_max_f32_e32 v177, v177, v177
	v_max_f32_e32 v196, v196, v196
	v_max_f32_e32 v197, v197, v197
	v_max_f32_e32 v198, v198, v198
	v_max_f32_e32 v199, v199, v199
	v_max_f32_e32 v200, v200, v200
	v_max_f32_e32 v201, v201, v201
	v_max_f32_e32 v202, v202, v202
	v_max_f32_e32 v203, v203, v203
	v_med3_f32 v170, v170, s20, v13
	v_med3_f32 v171, v171, s20, v13
	v_med3_f32 v172, v172, s20, v13
	v_med3_f32 v173, v173, s20, v13
	v_med3_f32 v174, v174, s20, v13
	v_med3_f32 v175, v175, s20, v13
	v_med3_f32 v176, v176, s20, v13
	v_med3_f32 v177, v177, s20, v13
	v_med3_f32 v196, v196, s20, v13
	v_med3_f32 v197, v197, s20, v13
	v_med3_f32 v198, v198, s20, v13
	v_med3_f32 v199, v199, s20, v13
	v_med3_f32 v200, v200, s20, v13
	v_med3_f32 v201, v201, s20, v13
	v_med3_f32 v202, v202, s20, v13
	v_med3_f32 v203, v203, s20, v13
	v_mov_b32_e32 v208, 0
	v_mov_b32_e32 v209, 0
	v_mov_b32_e32 v210, 0
	v_mov_b32_e32 v211, 0
	v_cvt_pk_fp8_f32 v208, v170, v171
	v_cvt_pk_fp8_f32 v209, v174, v175
	v_cvt_pk_fp8_f32 v210, v196, v197
	v_cvt_pk_fp8_f32 v211, v200, v201
	v_cvt_pk_fp8_f32 v208, v172, v173 op_sel:[0,0,1]
	v_cvt_pk_fp8_f32 v209, v176, v177 op_sel:[0,0,1]
	v_cvt_pk_fp8_f32 v210, v198, v199 op_sel:[0,0,1]
	v_cvt_pk_fp8_f32 v211, v202, v203 op_sel:[0,0,1]
	s_nop 0
	global_store_dwordx4 v11, v[208:211], s[14:15]
	ds_read_b32 v170, v9
	ds_read_b32 v171, v9 offset:512
	ds_read_b32 v172, v9 offset:1024
	ds_read_b32 v173, v9 offset:1536
	ds_read_b32 v174, v9 offset:2048
	ds_read_b32 v175, v9 offset:2560
	ds_read_b32 v176, v9 offset:3072
	ds_read_b32 v177, v9 offset:3584
	ds_read_b32 v196, v9 offset:4096
	ds_read_b32 v197, v9 offset:4608
	ds_read_b32 v198, v9 offset:5120
	ds_read_b32 v199, v9 offset:5632
	ds_read_b32 v200, v9 offset:6144
	ds_read_b32 v201, v9 offset:6656
	ds_read_b32 v202, v9 offset:7168
	ds_read_b32 v203, v9 offset:7680
	s_waitcnt lgkmcnt(0)
	v_max_f32_e32 v170, v170, v170
	v_max_f32_e32 v171, v171, v171
	v_max_f32_e32 v172, v172, v172
	v_max_f32_e32 v173, v173, v173
	v_max_f32_e32 v174, v174, v174
	v_max_f32_e32 v175, v175, v175
	v_max_f32_e32 v176, v176, v176
	v_max_f32_e32 v177, v177, v177
	v_max_f32_e32 v196, v196, v196
	v_max_f32_e32 v197, v197, v197
	v_max_f32_e32 v198, v198, v198
	v_max_f32_e32 v199, v199, v199
	v_max_f32_e32 v200, v200, v200
	v_max_f32_e32 v201, v201, v201
	v_max_f32_e32 v202, v202, v202
	v_max_f32_e32 v203, v203, v203
	v_med3_f32 v170, v170, s20, v13
	v_med3_f32 v171, v171, s20, v13
	v_med3_f32 v172, v172, s20, v13
	v_med3_f32 v173, v173, s20, v13
	v_med3_f32 v174, v174, s20, v13
	v_med3_f32 v175, v175, s20, v13
	v_med3_f32 v176, v176, s20, v13
	v_med3_f32 v177, v177, s20, v13
	v_med3_f32 v196, v196, s20, v13
	v_med3_f32 v197, v197, s20, v13
	v_med3_f32 v198, v198, s20, v13
	v_med3_f32 v199, v199, s20, v13
	v_med3_f32 v200, v200, s20, v13
	v_med3_f32 v201, v201, s20, v13
	v_med3_f32 v202, v202, s20, v13
	v_med3_f32 v203, v203, s20, v13
	v_mov_b32_e32 v208, 0
	v_mov_b32_e32 v209, 0
	v_mov_b32_e32 v210, 0
	v_mov_b32_e32 v211, 0
	v_cvt_pk_fp8_f32 v208, v170, v171
	v_cvt_pk_fp8_f32 v209, v174, v175
	v_cvt_pk_fp8_f32 v210, v196, v197
	v_cvt_pk_fp8_f32 v211, v200, v201
	v_cvt_pk_fp8_f32 v208, v172, v173 op_sel:[0,0,1]
	v_cvt_pk_fp8_f32 v209, v176, v177 op_sel:[0,0,1]
	v_cvt_pk_fp8_f32 v210, v198, v199 op_sel:[0,0,1]
	v_cvt_pk_fp8_f32 v211, v202, v203 op_sel:[0,0,1]
	s_nop 0
	global_store_dwordx4 v12, v[208:211], s[14:15]
	s_waitcnt vmcnt(32)
	v_mul_f32_e32 v100, 0x43000000, v100
	v_mul_f32_e32 v101, 0x43000000, v101
	v_mul_f32_e32 v102, 0x43000000, v102
	v_mul_f32_e32 v103, 0x43000000, v103
	ds_write_b128 v4, v[100:103]
	v_mul_f32_e32 v104, 0x43000000, v104
	v_mul_f32_e32 v105, 0x43000000, v105
	v_mul_f32_e32 v106, 0x43000000, v106
	v_mul_f32_e32 v107, 0x43000000, v107
	ds_write_b128 v4, v[104:107] offset:1024
	v_mul_f32_e32 v108, 0x43000000, v108
	v_mul_f32_e32 v109, 0x43000000, v109
	v_mul_f32_e32 v110, 0x43000000, v110
	v_mul_f32_e32 v111, 0x43000000, v111
	ds_write_b128 v4, v[108:111] offset:2048
	v_mul_f32_e32 v112, 0x43000000, v112
	v_mul_f32_e32 v113, 0x43000000, v113
	v_mul_f32_e32 v114, 0x43000000, v114
	v_mul_f32_e32 v115, 0x43000000, v115
	ds_write_b128 v4, v[112:115] offset:3072
	v_mul_f32_e32 v116, 0x43000000, v116
	v_mul_f32_e32 v117, 0x43000000, v117
	v_mul_f32_e32 v118, 0x43000000, v118
	v_mul_f32_e32 v119, 0x43000000, v119
	ds_write_b128 v4, v[116:119] offset:4096
	v_mul_f32_e32 v120, 0x43000000, v120
	v_mul_f32_e32 v121, 0x43000000, v121
	v_mul_f32_e32 v122, 0x43000000, v122
	v_mul_f32_e32 v123, 0x43000000, v123
	ds_write_b128 v4, v[120:123] offset:5120
	v_mul_f32_e32 v124, 0x43000000, v124
	v_mul_f32_e32 v125, 0x43000000, v125
	v_mul_f32_e32 v126, 0x43000000, v126
	v_mul_f32_e32 v127, 0x43000000, v127
	ds_write_b128 v4, v[124:127] offset:6144
	v_mul_f32_e32 v128, 0x43000000, v128
	v_mul_f32_e32 v129, 0x43000000, v129
	v_mul_f32_e32 v130, 0x43000000, v130
	v_mul_f32_e32 v131, 0x43000000, v131
	ds_write_b128 v4, v[128:131] offset:7168
	s_waitcnt lgkmcnt(0)
	s_barrier
; #define GAS __attribute__((address_space(1)))
; #define LAS __attribute__((address_space(3)))
; #define LDS_WAIT() asm volatile("s_waitcnt lgkmcnt(0)" ::: "memory")
;     const int pr = item >> 1, kb = 2 * (pr / nblk) + (item & 1), nb = pr % nblk, k0 = 64 * kb, n0 = 32 * nb;
;     const int nr = n0 + (lane & 31); const int sc = MAP == 1 ? src_col_in(nr) : nr;
;     float v[32];
; #pragma unroll
;     for (int i = 0; i < 32; ++i) v[i] = sc >= 0 ? W[(size_t)(k0 + 2 * i + (lane >> 5)) * Nsrc + sc] : 0.f;
; #pragma unroll
;     for (int i = 0; i < 32; ++i) { const int k = k0 + 2 * i + (lane >> 5); float x = v[i] * wscale; if (KS) x *= (k < ksplit ? ksA[k] : ksB[k - ksplit]); scr[(2 * i + (lane >> 5)) * 33 + (lane & 31)] = x; }
;     LDS_WAIT(); asm volatile("" ::: "memory");
;     const int c = lane & 7;
; #pragma unroll
;     for (int j = 0; j < 4; ++j) { const int n = (lane >> 3) + 8 * j; const LAS float* s = scr + (8 * c) * 33 + n;
;         const unsigned long long o = (unsigned long long)pg8::pk4_fp8(s[0 * 33], s[1 * 33], s[2 * 33], s[3 * 33]) | ((unsigned long long)pg8::pk4_fp8(s[4 * 33], s[5 * 33], s[6 * 33], s[7 * 33]) << 32);
;         *(GAS unsigned long long*)(WT + (size_t)(n0 + n) * K + k0 + 8 * c) = o; }
;     LDS_WAIT(); asm volatile("" ::: "memory");
; }
; __global__ void __launch_bounds__(NWAVES * 64, 2) hybrid_fwd(Args args) {
;     ...
;             if (r < I_O) { if (l >= WO_F8_FROM) p0_transpose_item_f8<true>(args.in[13] + (size_t)l * DM * DM, DM, DM, DM / 32, (unsigned char*)(ws + WS_WO + l * SZ_WO), 64.f, args.in[6] + l * 2048, args.in[12] + l * 2048, 2048, scr, r, lane);
	s_add_i32 s19, s39, 9
	s_min_u32 s19, s19, 31
	s_lshl_b32 s19, s19, 9
	s_add_u32 s12, s22, s19
	s_addc_u32 s13, s23, 0
	global_load_dwordx4 v[100:103], v10, s[12:13]
	s_add_u32 s12, s12, 0x8000
	s_addc_u32 s13, s13, 0
	global_load_dwordx4 v[104:107], v10, s[12:13]
	s_add_u32 s12, s12, 0x8000
	s_addc_u32 s13, s13, 0
	global_load_dwordx4 v[108:111], v10, s[12:13]
	s_add_u32 s12, s12, 0x8000
	s_addc_u32 s13, s13, 0
	global_load_dwordx4 v[112:115], v10, s[12:13]
	s_add_u32 s12, s12, 0x8000
	s_addc_u32 s13, s13, 0
	global_load_dwordx4 v[116:119], v10, s[12:13]
	s_add_u32 s12, s12, 0x8000
	s_addc_u32 s13, s13, 0
	global_load_dwordx4 v[120:123], v10, s[12:13]
	s_add_u32 s12, s12, 0x8000
	s_addc_u32 s13, s13, 0
	global_load_dwordx4 v[124:127], v10, s[12:13]
	s_add_u32 s12, s12, 0x8000
	s_addc_u32 s13, s13, 0
	global_load_dwordx4 v[128:131], v10, s[12:13]
	s_add_i32 s17, s16, 4032
	s_min_u32 s17, s17, 0xfff
	s_lshr_b32 s18, s17, 5
	s_add_i32 s18, s18, 0
	s_and_b32 s19, s17, 31
	s_lshl_b32 s19, s19, 21
	s_lshl_b32 s18, s18, 7
	s_add_u32 s18, s18, s19
	s_add_u32 s14, s4, s18
	s_addc_u32 s15, s5, 0
	ds_read_b32 v170, v6
	ds_read_b32 v171, v6 offset:512
	ds_read_b32 v172, v6 offset:1024
	ds_read_b32 v173, v6 offset:1536
	ds_read_b32 v174, v6 offset:2048
	ds_read_b32 v175, v6 offset:2560
	ds_read_b32 v176, v6 offset:3072
	ds_read_b32 v177, v6 offset:3584
	ds_read_b32 v196, v6 offset:4096
	ds_read_b32 v197, v6 offset:4608
	ds_read_b32 v198, v6 offset:5120
	ds_read_b32 v199, v6 offset:5632
	ds_read_b32 v200, v6 offset:6144
	ds_read_b32 v201, v6 offset:6656
	ds_read_b32 v202, v6 offset:7168
	ds_read_b32 v203, v6 offset:7680
	s_waitcnt lgkmcnt(0)
	v_max_f32_e32 v170, v170, v170
	v_max_f32_e32 v171, v171, v171
	v_max_f32_e32 v172, v172, v172
	v_max_f32_e32 v173, v173, v173
	v_max_f32_e32 v174, v174, v174
	v_max_f32_e32 v175, v175, v175
	v_max_f32_e32 v176, v176, v176
	v_max_f32_e32 v177, v177, v177
	v_max_f32_e32 v196, v196, v196
	v_max_f32_e32 v197, v197, v197
	v_max_f32_e32 v198, v198, v198
	v_max_f32_e32 v199, v199, v199
	v_max_f32_e32 v200, v200, v200
	v_max_f32_e32 v201, v201, v201
	v_max_f32_e32 v202, v202, v202
	v_max_f32_e32 v203, v203, v203
	v_med3_f32 v170, v170, s20, v13
	v_med3_f32 v171, v171, s20, v13
	v_med3_f32 v172, v172, s20, v13
	v_med3_f32 v173, v173, s20, v13
	v_med3_f32 v174, v174, s20, v13
	v_med3_f32 v175, v175, s20, v13
	v_med3_f32 v176, v176, s20, v13
	v_med3_f32 v177, v177, s20, v13
	v_med3_f32 v196, v196, s20, v13
	v_med3_f32 v197, v197, s20, v13
	v_med3_f32 v198, v198, s20, v13
	v_med3_f32 v199, v199, s20, v13
	v_med3_f32 v200, v200, s20, v13
	v_med3_f32 v201, v201, s20, v13
	v_med3_f32 v202, v202, s20, v13
	v_med3_f32 v203, v203, s20, v13
	v_mov_b32_e32 v208, 0
	v_mov_b32_e32 v209, 0
	v_mov_b32_e32 v210, 0
	v_mov_b32_e32 v211, 0
	v_cvt_pk_fp8_f32 v208, v170, v171
	v_cvt_pk_fp8_f32 v209, v174, v175
	v_cvt_pk_fp8_f32 v210, v196, v197
	v_cvt_pk_fp8_f32 v211, v200, v201
	v_cvt_pk_fp8_f32 v208, v172, v173 op_sel:[0,0,1]
	v_cvt_pk_fp8_f32 v209, v176, v177 op_sel:[0,0,1]
	v_cvt_pk_fp8_f32 v210, v198, v199 op_sel:[0,0,1]
	v_cvt_pk_fp8_f32 v211, v202, v203 op_sel:[0,0,1]
	s_nop 0
	global_store_dwordx4 v11, v[208:211], s[14:15]
	ds_read_b32 v170, v8
	ds_read_b32 v171, v8 offset:512
	ds_read_b32 v172, v8 offset:1024
	ds_read_b32 v173, v8 offset:1536
	ds_read_b32 v174, v8 offset:2048
	ds_read_b32 v175, v8 offset:2560
	ds_read_b32 v176, v8 offset:3072
	ds_read_b32 v177, v8 offset:3584
	ds_read_b32 v196, v8 offset:4096
	ds_read_b32 v197, v8 offset:4608
	ds_read_b32 v198, v8 offset:5120
	ds_read_b32 v199, v8 offset:5632
	ds_read_b32 v200, v8 offset:6144
	ds_read_b32 v201, v8 offset:6656
	ds_read_b32 v202, v8 offset:7168
	ds_read_b32 v203, v8 offset:7680
	s_waitcnt lgkmcnt(0)
	v_max_f32_e32 v170, v170, v170
	v_max_f32_e32 v171, v171, v171
	v_max_f32_e32 v172, v172, v172
	v_max_f32_e32 v173, v173, v173
	v_max_f32_e32 v174, v174, v174
	v_max_f32_e32 v175, v175, v175
	v_max_f32_e32 v176, v176, v176
	v_max_f32_e32 v177, v177, v177
	v_max_f32_e32 v196, v196, v196
	v_max_f32_e32 v197, v197, v197
	v_max_f32_e32 v198, v198, v198
	v_max_f32_e32 v199, v199, v199
	v_max_f32_e32 v200, v200, v200
	v_max_f32_e32 v201, v201, v201
	v_max_f32_e32 v202, v202, v202
	v_max_f32_e32 v203, v203, v203
	v_med3_f32 v170, v170, s20, v13
	v_med3_f32 v171, v171, s20, v13
	v_med3_f32 v172, v172, s20, v13
	v_med3_f32 v173, v173, s20, v13
	v_med3_f32 v174, v174, s20, v13
	v_med3_f32 v175, v175, s20, v13
	v_med3_f32 v176, v176, s20, v13
	v_med3_f32 v177, v177, s20, v13
	v_med3_f32 v196, v196, s20, v13
	v_med3_f32 v197, v197, s20, v13
	v_med3_f32 v198, v198, s20, v13
	v_med3_f32 v199, v199, s20, v13
	v_med3_f32 v200, v200, s20, v13
	v_med3_f32 v201, v201, s20, v13
	v_med3_f32 v202, v202, s20, v13
	v_med3_f32 v203, v203, s20, v13
	v_mov_b32_e32 v208, 0
	v_mov_b32_e32 v209, 0
	v_mov_b32_e32 v210, 0
	v_mov_b32_e32 v211, 0
	v_cvt_pk_fp8_f32 v208, v170, v171
	v_cvt_pk_fp8_f32 v209, v174, v175
	v_cvt_pk_fp8_f32 v210, v196, v197
	v_cvt_pk_fp8_f32 v211, v200, v201
	v_cvt_pk_fp8_f32 v208, v172, v173 op_sel:[0,0,1]
	v_cvt_pk_fp8_f32 v209, v176, v177 op_sel:[0,0,1]
	v_cvt_pk_fp8_f32 v210, v198, v199 op_sel:[0,0,1]
	v_cvt_pk_fp8_f32 v211, v202, v203 op_sel:[0,0,1]
	s_nop 0
	global_store_dwordx4 v12, v[208:211], s[14:15]
	s_waitcnt vmcnt(32)
	v_mul_f32_e32 v132, v20, v132
	v_mul_f32_e32 v133, v20, v133
	v_mul_f32_e32 v134, v20, v134
	v_mul_f32_e32 v135, v20, v135
	ds_write_b128 v5, v[132:135]
	v_mul_f32_e32 v136, v21, v136
	v_mul_f32_e32 v137, v21, v137
	v_mul_f32_e32 v138, v21, v138
	v_mul_f32_e32 v139, v21, v139
	ds_write_b128 v5, v[136:139] offset:1024
	v_mul_f32_e32 v140, v22, v140
	v_mul_f32_e32 v141, v22, v141
	v_mul_f32_e32 v142, v22, v142
	v_mul_f32_e32 v143, v22, v143
	ds_write_b128 v5, v[140:143] offset:2048
	v_mul_f32_e32 v144, v23, v144
	v_mul_f32_e32 v145, v23, v145
	v_mul_f32_e32 v146, v23, v146
	v_mul_f32_e32 v147, v23, v147
	ds_write_b128 v5, v[144:147] offset:3072
	v_mul_f32_e32 v148, v24, v148
	v_mul_f32_e32 v149, v24, v149
	v_mul_f32_e32 v150, v24, v150
	v_mul_f32_e32 v151, v24, v151
	ds_write_b128 v5, v[148:151] offset:4096
	v_mul_f32_e32 v152, v25, v152
	v_mul_f32_e32 v153, v25, v153
	v_mul_f32_e32 v154, v25, v154
	v_mul_f32_e32 v155, v25, v155
	ds_write_b128 v5, v[152:155] offset:5120
	v_mul_f32_e32 v156, v26, v156
	v_mul_f32_e32 v157, v26, v157
	v_mul_f32_e32 v158, v26, v158
	v_mul_f32_e32 v159, v26, v159
	ds_write_b128 v5, v[156:159] offset:6144
	v_mul_f32_e32 v160, v27, v160
	v_mul_f32_e32 v161, v27, v161
	v_mul_f32_e32 v162, v27, v162
	v_mul_f32_e32 v163, v27, v163
	ds_write_b128 v5, v[160:163] offset:7168
	s_waitcnt lgkmcnt(0)
	s_barrier
; #define GAS __attribute__((address_space(1)))
; #define LAS __attribute__((address_space(3)))
; #define LDS_WAIT() asm volatile("s_waitcnt lgkmcnt(0)" ::: "memory")
;     const int pr = item >> 1, kb = 2 * (pr / nblk) + (item & 1), nb = pr % nblk, k0 = 64 * kb, n0 = 32 * nb;
;     const int nr = n0 + (lane & 31); const int sc = MAP == 1 ? src_col_in(nr) : nr;
;     float v[32];
; #pragma unroll
;     for (int i = 0; i < 32; ++i) v[i] = sc >= 0 ? W[(size_t)(k0 + 2 * i + (lane >> 5)) * Nsrc + sc] : 0.f;
; #pragma unroll
;     for (int i = 0; i < 32; ++i) { const int k = k0 + 2 * i + (lane >> 5); float x = v[i] * wscale; if (KS) x *= (k < ksplit ? ksA[k] : ksB[k - ksplit]); scr[(2 * i + (lane >> 5)) * 33 + (lane & 31)] = x; }
;     LDS_WAIT(); asm volatile("" ::: "memory");
;     const int c = lane & 7;
; #pragma unroll
;     for (int j = 0; j < 4; ++j) { const int n = (lane >> 3) + 8 * j; const LAS float* s = scr + (8 * c) * 33 + n;
;         const unsigned long long o = (unsigned long long)pg8::pk4_fp8(s[0 * 33], s[1 * 33], s[2 * 33], s[3 * 33]) | ((unsigned long long)pg8::pk4_fp8(s[4 * 33], s[5 * 33], s[6 * 33], s[7 * 33]) << 32);
;         *(GAS unsigned long long*)(WT + (size_t)(n0 + n) * K + k0 + 8 * c) = o; }
;     LDS_WAIT(); asm volatile("" ::: "memory");
; }
; __global__ void __launch_bounds__(NWAVES * 64, 2) hybrid_fwd(Args args) {
;     ...
;             if (r < I_O) { if (l >= WO_F8_FROM) p0_transpose_item_f8<true>(args.in[13] + (size_t)l * DM * DM, DM, DM, DM / 32, (unsigned char*)(ws + WS_WO + l * SZ_WO), 64.f, args.in[6] + l * 2048, args.in[12] + l * 2048, 2048, scr, r, lane);
	s_add_i32 s19, s39, 12
	s_min_u32 s19, s19, 31
	s_lshl_b32 s19, s19, 9
	s_add_u32 s12, s22, s19
	s_addc_u32 s13, s23, 0
	global_load_dwordx4 v[132:135], v10, s[12:13]
	s_add_u32 s12, s12, 0x8000
	s_addc_u32 s13, s13, 0
	global_load_dwordx4 v[136:139], v10, s[12:13]
	s_add_u32 s12, s12, 0x8000
	s_addc_u32 s13, s13, 0
	global_load_dwordx4 v[140:143], v10, s[12:13]
	s_add_u32 s12, s12, 0x8000
	s_addc_u32 s13, s13, 0
	global_load_dwordx4 v[144:147], v10, s[12:13]
	s_add_u32 s12, s12, 0x8000
	s_addc_u32 s13, s13, 0
	global_load_dwordx4 v[148:151], v10, s[12:13]
	s_add_u32 s12, s12, 0x8000
	s_addc_u32 s13, s13, 0
	global_load_dwordx4 v[152:155], v10, s[12:13]
	s_add_u32 s12, s12, 0x8000
	s_addc_u32 s13, s13, 0
	global_load_dwordx4 v[156:159], v10, s[12:13]
	s_add_u32 s12, s12, 0x8000
	s_addc_u32 s13, s13, 0
	global_load_dwordx4 v[160:163], v10, s[12:13]
	s_add_i32 s19, s39, 0
	s_min_u32 s19, s19, 31
	s_lshl_b32 s19, s19, 19
	s_add_u32 s14, s50, s19
	s_addc_u32 s15, s51, 0
	ds_read_b32 v170, v7
	ds_read_b32 v171, v7 offset:512
	ds_read_b32 v172, v7 offset:1024
	ds_read_b32 v173, v7 offset:1536
	ds_read_b32 v174, v7 offset:2048
	ds_read_b32 v175, v7 offset:2560
	ds_read_b32 v176, v7 offset:3072
	ds_read_b32 v177, v7 offset:3584
	ds_read_b32 v196, v7 offset:4096
	ds_read_b32 v197, v7 offset:4608
	ds_read_b32 v198, v7 offset:5120
	ds_read_b32 v199, v7 offset:5632
	ds_read_b32 v200, v7 offset:6144
	ds_read_b32 v201, v7 offset:6656
	ds_read_b32 v202, v7 offset:7168
	ds_read_b32 v203, v7 offset:7680
	s_waitcnt lgkmcnt(0)
	v_max_f32_e32 v170, v170, v170
	v_max_f32_e32 v171, v171, v171
	v_max_f32_e32 v172, v172, v172
	v_max_f32_e32 v173, v173, v173
	v_max_f32_e32 v174, v174, v174
	v_max_f32_e32 v175, v175, v175
	v_max_f32_e32 v176, v176, v176
	v_max_f32_e32 v177, v177, v177
	v_max_f32_e32 v196, v196, v196
	v_max_f32_e32 v197, v197, v197
	v_max_f32_e32 v198, v198, v198
	v_max_f32_e32 v199, v199, v199
	v_max_f32_e32 v200, v200, v200
	v_max_f32_e32 v201, v201, v201
	v_max_f32_e32 v202, v202, v202
	v_max_f32_e32 v203, v203, v203
	v_med3_f32 v170, v170, s20, v13
	v_med3_f32 v171, v171, s20, v13
	v_med3_f32 v172, v172, s20, v13
	v_med3_f32 v173, v173, s20, v13
	v_med3_f32 v174, v174, s20, v13
	v_med3_f32 v175, v175, s20, v13
	v_med3_f32 v176, v176, s20, v13
	v_med3_f32 v177, v177, s20, v13
	v_med3_f32 v196, v196, s20, v13
	v_med3_f32 v197, v197, s20, v13
	v_med3_f32 v198, v198, s20, v13
	v_med3_f32 v199, v199, s20, v13
	v_med3_f32 v200, v200, s20, v13
	v_med3_f32 v201, v201, s20, v13
	v_med3_f32 v202, v202, s20, v13
	v_med3_f32 v203, v203, s20, v13
	v_mov_b32_e32 v208, 0
	v_mov_b32_e32 v209, 0
	v_mov_b32_e32 v210, 0
	v_mov_b32_e32 v211, 0
	v_cvt_pk_fp8_f32 v208, v170, v171
	v_cvt_pk_fp8_f32 v209, v174, v175
	v_cvt_pk_fp8_f32 v210, v196, v197
	v_cvt_pk_fp8_f32 v211, v200, v201
	v_cvt_pk_fp8_f32 v208, v172, v173 op_sel:[0,0,1]
	v_cvt_pk_fp8_f32 v209, v176, v177 op_sel:[0,0,1]
	v_cvt_pk_fp8_f32 v210, v198, v199 op_sel:[0,0,1]
	v_cvt_pk_fp8_f32 v211, v202, v203 op_sel:[0,0,1]
	s_nop 0
	global_store_dwordx4 v28, v[208:211], s[14:15]
	ds_read_b32 v170, v9
	ds_read_b32 v171, v9 offset:512
	ds_read_b32 v172, v9 offset:1024
	ds_read_b32 v173, v9 offset:1536
	ds_read_b32 v174, v9 offset:2048
	ds_read_b32 v175, v9 offset:2560
	ds_read_b32 v176, v9 offset:3072
	ds_read_b32 v177, v9 offset:3584
	ds_read_b32 v196, v9 offset:4096
	ds_read_b32 v197, v9 offset:4608
	ds_read_b32 v198, v9 offset:5120
	ds_read_b32 v199, v9 offset:5632
	ds_read_b32 v200, v9 offset:6144
	ds_read_b32 v201, v9 offset:6656
	ds_read_b32 v202, v9 offset:7168
	ds_read_b32 v203, v9 offset:7680
	s_waitcnt lgkmcnt(0)
	v_max_f32_e32 v170, v170, v170
	v_max_f32_e32 v171, v171, v171
	v_max_f32_e32 v172, v172, v172
	v_max_f32_e32 v173, v173, v173
	v_max_f32_e32 v174, v174, v174
	v_max_f32_e32 v175, v175, v175
	v_max_f32_e32 v176, v176, v176
	v_max_f32_e32 v177, v177, v177
	v_max_f32_e32 v196, v196, v196
	v_max_f32_e32 v197, v197, v197
	v_max_f32_e32 v198, v198, v198
	v_max_f32_e32 v199, v199, v199
	v_max_f32_e32 v200, v200, v200
	v_max_f32_e32 v201, v201, v201
	v_max_f32_e32 v202, v202, v202
	v_max_f32_e32 v203, v203, v203
	v_med3_f32 v170, v170, s20, v13
	v_med3_f32 v171, v171, s20, v13
	v_med3_f32 v172, v172, s20, v13
	v_med3_f32 v173, v173, s20, v13
	v_med3_f32 v174, v174, s20, v13
	v_med3_f32 v175, v175, s20, v13
	v_med3_f32 v176, v176, s20, v13
	v_med3_f32 v177, v177, s20, v13
	v_med3_f32 v196, v196, s20, v13
	v_med3_f32 v197, v197, s20, v13
	v_med3_f32 v198, v198, s20, v13
	v_med3_f32 v199, v199, s20, v13
	v_med3_f32 v200, v200, s20, v13
	v_med3_f32 v201, v201, s20, v13
	v_med3_f32 v202, v202, s20, v13
	v_med3_f32 v203, v203, s20, v13
	v_mov_b32_e32 v208, 0
	v_mov_b32_e32 v209, 0
	v_mov_b32_e32 v210, 0
	v_mov_b32_e32 v211, 0
	v_cvt_pk_fp8_f32 v208, v170, v171
	v_cvt_pk_fp8_f32 v209, v174, v175
	v_cvt_pk_fp8_f32 v210, v196, v197
	v_cvt_pk_fp8_f32 v211, v200, v201
	v_cvt_pk_fp8_f32 v208, v172, v173 op_sel:[0,0,1]
	v_cvt_pk_fp8_f32 v209, v176, v177 op_sel:[0,0,1]
	v_cvt_pk_fp8_f32 v210, v198, v199 op_sel:[0,0,1]
	v_cvt_pk_fp8_f32 v211, v202, v203 op_sel:[0,0,1]
	s_nop 0
	global_store_dwordx4 v29, v[208:211], s[14:15]
	s_waitcnt vmcnt(32)
	v_mul_f32_e32 v36, v20, v36
	v_mul_f32_e32 v37, v20, v37
	v_mul_f32_e32 v38, v20, v38
	v_mul_f32_e32 v39, v20, v39
	ds_write_b128 v4, v[36:39]
	v_mul_f32_e32 v40, v21, v40
	v_mul_f32_e32 v41, v21, v41
	v_mul_f32_e32 v42, v21, v42
	v_mul_f32_e32 v43, v21, v43
	ds_write_b128 v4, v[40:43] offset:1024
	v_mul_f32_e32 v44, v22, v44
	v_mul_f32_e32 v45, v22, v45
	v_mul_f32_e32 v46, v22, v46
	v_mul_f32_e32 v47, v22, v47
	ds_write_b128 v4, v[44:47] offset:2048
	v_mul_f32_e32 v48, v23, v48
	v_mul_f32_e32 v49, v23, v49
	v_mul_f32_e32 v50, v23, v50
	v_mul_f32_e32 v51, v23, v51
	ds_write_b128 v4, v[48:51] offset:3072
	v_mul_f32_e32 v52, v24, v52
	v_mul_f32_e32 v53, v24, v53
	v_mul_f32_e32 v54, v24, v54
	v_mul_f32_e32 v55, v24, v55
	ds_write_b128 v4, v[52:55] offset:4096
	v_mul_f32_e32 v56, v25, v56
	v_mul_f32_e32 v57, v25, v57
	v_mul_f32_e32 v58, v25, v58
	v_mul_f32_e32 v59, v25, v59
	ds_write_b128 v4, v[56:59] offset:5120
	v_mul_f32_e32 v60, v26, v60
	v_mul_f32_e32 v61, v26, v61
	v_mul_f32_e32 v62, v26, v62
	v_mul_f32_e32 v63, v26, v63
	ds_write_b128 v4, v[60:63] offset:6144
	v_mul_f32_e32 v64, v27, v64
	v_mul_f32_e32 v65, v27, v65
	v_mul_f32_e32 v66, v27, v66
	v_mul_f32_e32 v67, v27, v67
	ds_write_b128 v4, v[64:67] offset:7168
	s_waitcnt lgkmcnt(0)
	s_barrier
; #define GAS __attribute__((address_space(1)))
; #define LAS __attribute__((address_space(3)))
; #define LDS_WAIT() asm volatile("s_waitcnt lgkmcnt(0)" ::: "memory")
;     const int pr = item >> 1, kb = 2 * (pr / nblk) + (item & 1), nb = pr % nblk, k0 = 64 * kb, n0 = 32 * nb;
;     const int nr = n0 + (lane & 31); const int sc = MAP == 1 ? src_col_in(nr) : nr;
;     float v[32];
; #pragma unroll
;     for (int i = 0; i < 32; ++i) v[i] = sc >= 0 ? W[(size_t)(k0 + 2 * i + (lane >> 5)) * Nsrc + sc] : 0.f;
; #pragma unroll
;     for (int i = 0; i < 32; ++i) { const int k = k0 + 2 * i + (lane >> 5); float x = v[i] * wscale; if (KS) x *= (k < ksplit ? ksA[k] : ksB[k - ksplit]); scr[(2 * i + (lane >> 5)) * 33 + (lane & 31)] = x; }
;     LDS_WAIT(); asm volatile("" ::: "memory");
;     const int c = lane & 7;
; #pragma unroll
;     for (int j = 0; j < 4; ++j) { const int n = (lane >> 3) + 8 * j; const LAS float* s = scr + (8 * c) * 33 + n;
;         const unsigned long long o = (unsigned long long)pg8::pk4_fp8(s[0 * 33], s[1 * 33], s[2 * 33], s[3 * 33]) | ((unsigned long long)pg8::pk4_fp8(s[4 * 33], s[5 * 33], s[6 * 33], s[7 * 33]) << 32);
;         *(GAS unsigned long long*)(WT + (size_t)(n0 + n) * K + k0 + 8 * c) = o; }
;     LDS_WAIT(); asm volatile("" ::: "memory");
; }
; __global__ void __launch_bounds__(NWAVES * 64, 2) hybrid_fwd(Args args) {
;     ...
;             if (r < I_O) { if (l >= WO_F8_FROM) p0_transpose_item_f8<true>(args.in[13] + (size_t)l * DM * DM, DM, DM, DM / 32, (unsigned char*)(ws + WS_WO + l * SZ_WO), 64.f, args.in[6] + l * 2048, args.in[12] + l * 2048, 2048, scr, r, lane);
	s_add_i32 s19, s39, 15
	s_min_u32 s19, s19, 31
	s_lshl_b32 s19, s19, 9
	s_add_u32 s12, s22, s19
	s_addc_u32 s13, s23, 0
	global_load_dwordx4 v[36:39], v10, s[12:13]
	s_add_u32 s12, s12, 0x8000
	s_addc_u32 s13, s13, 0
	global_load_dwordx4 v[40:43], v10, s[12:13]
	s_add_u32 s12, s12, 0x8000
	s_addc_u32 s13, s13, 0
	global_load_dwordx4 v[44:47], v10, s[12:13]
	s_add_u32 s12, s12, 0x8000
	s_addc_u32 s13, s13, 0
	global_load_dwordx4 v[48:51], v10, s[12:13]
	s_add_u32 s12, s12, 0x8000
	s_addc_u32 s13, s13, 0
	global_load_dwordx4 v[52:55], v10, s[12:13]
	s_add_u32 s12, s12, 0x8000
	s_addc_u32 s13, s13, 0
	global_load_dwordx4 v[56:59], v10, s[12:13]
	s_add_u32 s12, s12, 0x8000
	s_addc_u32 s13, s13, 0
	global_load_dwordx4 v[60:63], v10, s[12:13]
	s_add_u32 s12, s12, 0x8000
	s_addc_u32 s13, s13, 0
	global_load_dwordx4 v[64:67], v10, s[12:13]
	s_add_i32 s19, s39, 3
	s_min_u32 s19, s19, 31
	s_lshl_b32 s19, s19, 19
	s_add_u32 s14, s50, s19
	s_addc_u32 s15, s51, 0
	ds_read_b32 v170, v6
	ds_read_b32 v171, v6 offset:512
	ds_read_b32 v172, v6 offset:1024
	ds_read_b32 v173, v6 offset:1536
	ds_read_b32 v174, v6 offset:2048
	ds_read_b32 v175, v6 offset:2560
	ds_read_b32 v176, v6 offset:3072
	ds_read_b32 v177, v6 offset:3584
	ds_read_b32 v196, v6 offset:4096
	ds_read_b32 v197, v6 offset:4608
	ds_read_b32 v198, v6 offset:5120
	ds_read_b32 v199, v6 offset:5632
	ds_read_b32 v200, v6 offset:6144
	ds_read_b32 v201, v6 offset:6656
	ds_read_b32 v202, v6 offset:7168
	ds_read_b32 v203, v6 offset:7680
	s_waitcnt lgkmcnt(0)
	v_max_f32_e32 v170, v170, v170
	v_max_f32_e32 v171, v171, v171
	v_max_f32_e32 v172, v172, v172
	v_max_f32_e32 v173, v173, v173
	v_max_f32_e32 v174, v174, v174
	v_max_f32_e32 v175, v175, v175
	v_max_f32_e32 v176, v176, v176
	v_max_f32_e32 v177, v177, v177
	v_max_f32_e32 v196, v196, v196
	v_max_f32_e32 v197, v197, v197
	v_max_f32_e32 v198, v198, v198
	v_max_f32_e32 v199, v199, v199
	v_max_f32_e32 v200, v200, v200
	v_max_f32_e32 v201, v201, v201
	v_max_f32_e32 v202, v202, v202
	v_max_f32_e32 v203, v203, v203
	v_med3_f32 v170, v170, s20, v13
	v_med3_f32 v171, v171, s20, v13
	v_med3_f32 v172, v172, s20, v13
	v_med3_f32 v173, v173, s20, v13
	v_med3_f32 v174, v174, s20, v13
	v_med3_f32 v175, v175, s20, v13
	v_med3_f32 v176, v176, s20, v13
	v_med3_f32 v177, v177, s20, v13
	v_med3_f32 v196, v196, s20, v13
	v_med3_f32 v197, v197, s20, v13
	v_med3_f32 v198, v198, s20, v13
	v_med3_f32 v199, v199, s20, v13
	v_med3_f32 v200, v200, s20, v13
	v_med3_f32 v201, v201, s20, v13
	v_med3_f32 v202, v202, s20, v13
	v_med3_f32 v203, v203, s20, v13
	v_mov_b32_e32 v208, 0
	v_mov_b32_e32 v209, 0
	v_mov_b32_e32 v210, 0
	v_mov_b32_e32 v211, 0
	v_cvt_pk_fp8_f32 v208, v170, v171
	v_cvt_pk_fp8_f32 v209, v174, v175
	v_cvt_pk_fp8_f32 v210, v196, v197
	v_cvt_pk_fp8_f32 v211, v200, v201
	v_cvt_pk_fp8_f32 v208, v172, v173 op_sel:[0,0,1]
	v_cvt_pk_fp8_f32 v209, v176, v177 op_sel:[0,0,1]
	v_cvt_pk_fp8_f32 v210, v198, v199 op_sel:[0,0,1]
	v_cvt_pk_fp8_f32 v211, v202, v203 op_sel:[0,0,1]
	s_nop 0
	global_store_dwordx4 v28, v[208:211], s[14:15]
	ds_read_b32 v170, v8
	ds_read_b32 v171, v8 offset:512
	ds_read_b32 v172, v8 offset:1024
	ds_read_b32 v173, v8 offset:1536
	ds_read_b32 v174, v8 offset:2048
	ds_read_b32 v175, v8 offset:2560
	ds_read_b32 v176, v8 offset:3072
	ds_read_b32 v177, v8 offset:3584
	ds_read_b32 v196, v8 offset:4096
	ds_read_b32 v197, v8 offset:4608
	ds_read_b32 v198, v8 offset:5120
	ds_read_b32 v199, v8 offset:5632
	ds_read_b32 v200, v8 offset:6144
	ds_read_b32 v201, v8 offset:6656
	ds_read_b32 v202, v8 offset:7168
	ds_read_b32 v203, v8 offset:7680
	s_waitcnt lgkmcnt(0)
	v_max_f32_e32 v170, v170, v170
	v_max_f32_e32 v171, v171, v171
	v_max_f32_e32 v172, v172, v172
	v_max_f32_e32 v173, v173, v173
	v_max_f32_e32 v174, v174, v174
	v_max_f32_e32 v175, v175, v175
	v_max_f32_e32 v176, v176, v176
	v_max_f32_e32 v177, v177, v177
	v_max_f32_e32 v196, v196, v196
	v_max_f32_e32 v197, v197, v197
	v_max_f32_e32 v198, v198, v198
	v_max_f32_e32 v199, v199, v199
	v_max_f32_e32 v200, v200, v200
	v_max_f32_e32 v201, v201, v201
	v_max_f32_e32 v202, v202, v202
	v_max_f32_e32 v203, v203, v203
	v_med3_f32 v170, v170, s20, v13
	v_med3_f32 v171, v171, s20, v13
	v_med3_f32 v172, v172, s20, v13
	v_med3_f32 v173, v173, s20, v13
	v_med3_f32 v174, v174, s20, v13
	v_med3_f32 v175, v175, s20, v13
	v_med3_f32 v176, v176, s20, v13
	v_med3_f32 v177, v177, s20, v13
	v_med3_f32 v196, v196, s20, v13
	v_med3_f32 v197, v197, s20, v13
	v_med3_f32 v198, v198, s20, v13
	v_med3_f32 v199, v199, s20, v13
	v_med3_f32 v200, v200, s20, v13
	v_med3_f32 v201, v201, s20, v13
	v_med3_f32 v202, v202, s20, v13
	v_med3_f32 v203, v203, s20, v13
	v_mov_b32_e32 v208, 0
	v_mov_b32_e32 v209, 0
	v_mov_b32_e32 v210, 0
	v_mov_b32_e32 v211, 0
	v_cvt_pk_fp8_f32 v208, v170, v171
	v_cvt_pk_fp8_f32 v209, v174, v175
	v_cvt_pk_fp8_f32 v210, v196, v197
	v_cvt_pk_fp8_f32 v211, v200, v201
	v_cvt_pk_fp8_f32 v208, v172, v173 op_sel:[0,0,1]
	v_cvt_pk_fp8_f32 v209, v176, v177 op_sel:[0,0,1]
	v_cvt_pk_fp8_f32 v210, v198, v199 op_sel:[0,0,1]
	v_cvt_pk_fp8_f32 v211, v202, v203 op_sel:[0,0,1]
	s_nop 0
	global_store_dwordx4 v29, v[208:211], s[14:15]
	s_waitcnt vmcnt(32)
	v_mul_f32_e32 v68, v20, v68
	v_mul_f32_e32 v69, v20, v69
	v_mul_f32_e32 v70, v20, v70
	v_mul_f32_e32 v71, v20, v71
	ds_write_b128 v5, v[68:71]
	v_mul_f32_e32 v72, v21, v72
	v_mul_f32_e32 v73, v21, v73
	v_mul_f32_e32 v74, v21, v74
	v_mul_f32_e32 v75, v21, v75
	ds_write_b128 v5, v[72:75] offset:1024
	v_mul_f32_e32 v76, v22, v76
	v_mul_f32_e32 v77, v22, v77
	v_mul_f32_e32 v78, v22, v78
	v_mul_f32_e32 v79, v22, v79
	ds_write_b128 v5, v[76:79] offset:2048
	v_mul_f32_e32 v80, v23, v80
	v_mul_f32_e32 v81, v23, v81
	v_mul_f32_e32 v82, v23, v82
	v_mul_f32_e32 v83, v23, v83
	ds_write_b128 v5, v[80:83] offset:3072
	v_mul_f32_e32 v84, v24, v84
	v_mul_f32_e32 v85, v24, v85
	v_mul_f32_e32 v86, v24, v86
	v_mul_f32_e32 v87, v24, v87
	ds_write_b128 v5, v[84:87] offset:4096
	v_mul_f32_e32 v88, v25, v88
	v_mul_f32_e32 v89, v25, v89
	v_mul_f32_e32 v90, v25, v90
	v_mul_f32_e32 v91, v25, v91
	ds_write_b128 v5, v[88:91] offset:5120
	v_mul_f32_e32 v92, v26, v92
	v_mul_f32_e32 v93, v26, v93
	v_mul_f32_e32 v94, v26, v94
	v_mul_f32_e32 v95, v26, v95
	ds_write_b128 v5, v[92:95] offset:6144
	v_mul_f32_e32 v96, v27, v96
	v_mul_f32_e32 v97, v27, v97
	v_mul_f32_e32 v98, v27, v98
	v_mul_f32_e32 v99, v27, v99
	ds_write_b128 v5, v[96:99] offset:7168
	s_waitcnt lgkmcnt(0)
	s_barrier
; #define GAS __attribute__((address_space(1)))
; #define LAS __attribute__((address_space(3)))
; #define LDS_WAIT() asm volatile("s_waitcnt lgkmcnt(0)" ::: "memory")
;     const int pr = item >> 1, kb = 2 * (pr / nblk) + (item & 1), nb = pr % nblk, k0 = 64 * kb, n0 = 32 * nb;
;     const int nr = n0 + (lane & 31); const int sc = MAP == 1 ? src_col_in(nr) : nr;
;     float v[32];
; #pragma unroll
;     for (int i = 0; i < 32; ++i) v[i] = sc >= 0 ? W[(size_t)(k0 + 2 * i + (lane >> 5)) * Nsrc + sc] : 0.f;
; #pragma unroll
;     for (int i = 0; i < 32; ++i) { const int k = k0 + 2 * i + (lane >> 5); float x = v[i] * wscale; if (KS) x *= (k < ksplit ? ksA[k] : ksB[k - ksplit]); scr[(2 * i + (lane >> 5)) * 33 + (lane & 31)] = x; }
;     LDS_WAIT(); asm volatile("" ::: "memory");
;     const int c = lane & 7;
; #pragma unroll
;     for (int j = 0; j < 4; ++j) { const int n = (lane >> 3) + 8 * j; const LAS float* s = scr + (8 * c) * 33 + n;
;         const unsigned long long o = (unsigned long long)pg8::pk4_fp8(s[0 * 33], s[1 * 33], s[2 * 33], s[3 * 33]) | ((unsigned long long)pg8::pk4_fp8(s[4 * 33], s[5 * 33], s[6 * 33], s[7 * 33]) << 32);
;         *(GAS unsigned long long*)(WT + (size_t)(n0 + n) * K + k0 + 8 * c) = o; }
;     LDS_WAIT(); asm volatile("" ::: "memory");
; }
; __global__ void __launch_bounds__(NWAVES * 64, 2) hybrid_fwd(Args args) {
;     ...
;             if (r < I_O) { if (l >= WO_F8_FROM) p0_transpose_item_f8<true>(args.in[13] + (size_t)l * DM * DM, DM, DM, DM / 32, (unsigned char*)(ws + WS_WO + l * SZ_WO), 64.f, args.in[6] + l * 2048, args.in[12] + l * 2048, 2048, scr, r, lane);
	s_add_i32 s19, s39, 18
	s_min_u32 s19, s19, 31
	s_lshl_b32 s19, s19, 9
	s_add_u32 s12, s22, s19
	s_addc_u32 s13, s23, 0
	global_load_dwordx4 v[68:71], v10, s[12:13]
	s_add_u32 s12, s12, 0x8000
	s_addc_u32 s13, s13, 0
	global_load_dwordx4 v[72:75], v10, s[12:13]
	s_add_u32 s12, s12, 0x8000
	s_addc_u32 s13, s13, 0
	global_load_dwordx4 v[76:79], v10, s[12:13]
	s_add_u32 s12, s12, 0x8000
	s_addc_u32 s13, s13, 0
	global_load_dwordx4 v[80:83], v10, s[12:13]
	s_add_u32 s12, s12, 0x8000
	s_addc_u32 s13, s13, 0
	global_load_dwordx4 v[84:87], v10, s[12:13]
	s_add_u32 s12, s12, 0x8000
	s_addc_u32 s13, s13, 0
	global_load_dwordx4 v[88:91], v10, s[12:13]
	s_add_u32 s12, s12, 0x8000
	s_addc_u32 s13, s13, 0
	global_load_dwordx4 v[92:95], v10, s[12:13]
	s_add_u32 s12, s12, 0x8000
	s_addc_u32 s13, s13, 0
	global_load_dwordx4 v[96:99], v10, s[12:13]
	s_add_i32 s19, s39, 6
	s_min_u32 s19, s19, 31
	s_lshl_b32 s19, s19, 19
	s_add_u32 s14, s50, s19
	s_addc_u32 s15, s51, 0
	ds_read_b32 v170, v7
	ds_read_b32 v171, v7 offset:512
	ds_read_b32 v172, v7 offset:1024
	ds_read_b32 v173, v7 offset:1536
	ds_read_b32 v174, v7 offset:2048
	ds_read_b32 v175, v7 offset:2560
	ds_read_b32 v176, v7 offset:3072
	ds_read_b32 v177, v7 offset:3584
	ds_read_b32 v196, v7 offset:4096
	ds_read_b32 v197, v7 offset:4608
	ds_read_b32 v198, v7 offset:5120
	ds_read_b32 v199, v7 offset:5632
	ds_read_b32 v200, v7 offset:6144
	ds_read_b32 v201, v7 offset:6656
	ds_read_b32 v202, v7 offset:7168
	ds_read_b32 v203, v7 offset:7680
	s_waitcnt lgkmcnt(0)
	v_max_f32_e32 v170, v170, v170
	v_max_f32_e32 v171, v171, v171
	v_max_f32_e32 v172, v172, v172
	v_max_f32_e32 v173, v173, v173
	v_max_f32_e32 v174, v174, v174
	v_max_f32_e32 v175, v175, v175
	v_max_f32_e32 v176, v176, v176
	v_max_f32_e32 v177, v177, v177
	v_max_f32_e32 v196, v196, v196
	v_max_f32_e32 v197, v197, v197
	v_max_f32_e32 v198, v198, v198
	v_max_f32_e32 v199, v199, v199
	v_max_f32_e32 v200, v200, v200
	v_max_f32_e32 v201, v201, v201
	v_max_f32_e32 v202, v202, v202
	v_max_f32_e32 v203, v203, v203
	v_med3_f32 v170, v170, s20, v13
	v_med3_f32 v171, v171, s20, v13
	v_med3_f32 v172, v172, s20, v13
	v_med3_f32 v173, v173, s20, v13
	v_med3_f32 v174, v174, s20, v13
	v_med3_f32 v175, v175, s20, v13
	v_med3_f32 v176, v176, s20, v13
	v_med3_f32 v177, v177, s20, v13
	v_med3_f32 v196, v196, s20, v13
	v_med3_f32 v197, v197, s20, v13
	v_med3_f32 v198, v198, s20, v13
	v_med3_f32 v199, v199, s20, v13
	v_med3_f32 v200, v200, s20, v13
	v_med3_f32 v201, v201, s20, v13
	v_med3_f32 v202, v202, s20, v13
	v_med3_f32 v203, v203, s20, v13
	v_mov_b32_e32 v208, 0
	v_mov_b32_e32 v209, 0
	v_mov_b32_e32 v210, 0
	v_mov_b32_e32 v211, 0
	v_cvt_pk_fp8_f32 v208, v170, v171
	v_cvt_pk_fp8_f32 v209, v174, v175
	v_cvt_pk_fp8_f32 v210, v196, v197
	v_cvt_pk_fp8_f32 v211, v200, v201
	v_cvt_pk_fp8_f32 v208, v172, v173 op_sel:[0,0,1]
	v_cvt_pk_fp8_f32 v209, v176, v177 op_sel:[0,0,1]
	v_cvt_pk_fp8_f32 v210, v198, v199 op_sel:[0,0,1]
	v_cvt_pk_fp8_f32 v211, v202, v203 op_sel:[0,0,1]
	s_nop 0
	global_store_dwordx4 v28, v[208:211], s[14:15]
	ds_read_b32 v170, v9
	ds_read_b32 v171, v9 offset:512
	ds_read_b32 v172, v9 offset:1024
	ds_read_b32 v173, v9 offset:1536
	ds_read_b32 v174, v9 offset:2048
	ds_read_b32 v175, v9 offset:2560
	ds_read_b32 v176, v9 offset:3072
	ds_read_b32 v177, v9 offset:3584
	ds_read_b32 v196, v9 offset:4096
	ds_read_b32 v197, v9 offset:4608
	ds_read_b32 v198, v9 offset:5120
	ds_read_b32 v199, v9 offset:5632
	ds_read_b32 v200, v9 offset:6144
	ds_read_b32 v201, v9 offset:6656
	ds_read_b32 v202, v9 offset:7168
	ds_read_b32 v203, v9 offset:7680
	s_waitcnt lgkmcnt(0)
	v_max_f32_e32 v170, v170, v170
	v_max_f32_e32 v171, v171, v171
	v_max_f32_e32 v172, v172, v172
	v_max_f32_e32 v173, v173, v173
	v_max_f32_e32 v174, v174, v174
	v_max_f32_e32 v175, v175, v175
	v_max_f32_e32 v176, v176, v176
	v_max_f32_e32 v177, v177, v177
	v_max_f32_e32 v196, v196, v196
	v_max_f32_e32 v197, v197, v197
	v_max_f32_e32 v198, v198, v198
	v_max_f32_e32 v199, v199, v199
	v_max_f32_e32 v200, v200, v200
	v_max_f32_e32 v201, v201, v201
	v_max_f32_e32 v202, v202, v202
	v_max_f32_e32 v203, v203, v203
	v_med3_f32 v170, v170, s20, v13
	v_med3_f32 v171, v171, s20, v13
	v_med3_f32 v172, v172, s20, v13
	v_med3_f32 v173, v173, s20, v13
	v_med3_f32 v174, v174, s20, v13
	v_med3_f32 v175, v175, s20, v13
	v_med3_f32 v176, v176, s20, v13
	v_med3_f32 v177, v177, s20, v13
	v_med3_f32 v196, v196, s20, v13
	v_med3_f32 v197, v197, s20, v13
	v_med3_f32 v198, v198, s20, v13
	v_med3_f32 v199, v199, s20, v13
	v_med3_f32 v200, v200, s20, v13
	v_med3_f32 v201, v201, s20, v13
	v_med3_f32 v202, v202, s20, v13
	v_med3_f32 v203, v203, s20, v13
	v_mov_b32_e32 v208, 0
	v_mov_b32_e32 v209, 0
	v_mov_b32_e32 v210, 0
	v_mov_b32_e32 v211, 0
	v_cvt_pk_fp8_f32 v208, v170, v171
	v_cvt_pk_fp8_f32 v209, v174, v175
	v_cvt_pk_fp8_f32 v210, v196, v197
	v_cvt_pk_fp8_f32 v211, v200, v201
	v_cvt_pk_fp8_f32 v208, v172, v173 op_sel:[0,0,1]
	v_cvt_pk_fp8_f32 v209, v176, v177 op_sel:[0,0,1]
	v_cvt_pk_fp8_f32 v210, v198, v199 op_sel:[0,0,1]
	v_cvt_pk_fp8_f32 v211, v202, v203 op_sel:[0,0,1]
	s_nop 0
	global_store_dwordx4 v29, v[208:211], s[14:15]
	s_waitcnt vmcnt(32)
	v_mul_f32_e32 v100, v20, v100
	v_mul_f32_e32 v101, v20, v101
	v_mul_f32_e32 v102, v20, v102
	v_mul_f32_e32 v103, v20, v103
	ds_write_b128 v4, v[100:103]
	v_mul_f32_e32 v104, v21, v104
	v_mul_f32_e32 v105, v21, v105
	v_mul_f32_e32 v106, v21, v106
	v_mul_f32_e32 v107, v21, v107
	ds_write_b128 v4, v[104:107] offset:1024
	v_mul_f32_e32 v108, v22, v108
	v_mul_f32_e32 v109, v22, v109
	v_mul_f32_e32 v110, v22, v110
	v_mul_f32_e32 v111, v22, v111
	ds_write_b128 v4, v[108:111] offset:2048
	v_mul_f32_e32 v112, v23, v112
	v_mul_f32_e32 v113, v23, v113
	v_mul_f32_e32 v114, v23, v114
	v_mul_f32_e32 v115, v23, v115
	ds_write_b128 v4, v[112:115] offset:3072
	v_mul_f32_e32 v116, v24, v116
	v_mul_f32_e32 v117, v24, v117
	v_mul_f32_e32 v118, v24, v118
	v_mul_f32_e32 v119, v24, v119
	ds_write_b128 v4, v[116:119] offset:4096
	v_mul_f32_e32 v120, v25, v120
	v_mul_f32_e32 v121, v25, v121
	v_mul_f32_e32 v122, v25, v122
	v_mul_f32_e32 v123, v25, v123
	ds_write_b128 v4, v[120:123] offset:5120
	v_mul_f32_e32 v124, v26, v124
	v_mul_f32_e32 v125, v26, v125
	v_mul_f32_e32 v126, v26, v126
	v_mul_f32_e32 v127, v26, v127
	ds_write_b128 v4, v[124:127] offset:6144
	v_mul_f32_e32 v128, v27, v128
	v_mul_f32_e32 v129, v27, v129
	v_mul_f32_e32 v130, v27, v130
	v_mul_f32_e32 v131, v27, v131
	ds_write_b128 v4, v[128:131] offset:7168
	s_waitcnt lgkmcnt(0)
	s_barrier
; #define GAS __attribute__((address_space(1)))
; #define LAS __attribute__((address_space(3)))
; #define LDS_WAIT() asm volatile("s_waitcnt lgkmcnt(0)" ::: "memory")
;     const int pr = item >> 1, kb = 2 * (pr / nblk) + (item & 1), nb = pr % nblk, k0 = 64 * kb, n0 = 32 * nb;
;     const int nr = n0 + (lane & 31); const int sc = MAP == 1 ? src_col_in(nr) : nr;
;     float v[32];
; #pragma unroll
;     for (int i = 0; i < 32; ++i) v[i] = sc >= 0 ? W[(size_t)(k0 + 2 * i + (lane >> 5)) * Nsrc + sc] : 0.f;
; #pragma unroll
;     for (int i = 0; i < 32; ++i) { const int k = k0 + 2 * i + (lane >> 5); float x = v[i] * wscale; if (KS) x *= (k < ksplit ? ksA[k] : ksB[k - ksplit]); scr[(2 * i + (lane >> 5)) * 33 + (lane & 31)] = x; }
;     LDS_WAIT(); asm volatile("" ::: "memory");
;     const int c = lane & 7;
; #pragma unroll
;     for (int j = 0; j < 4; ++j) { const int n = (lane >> 3) + 8 * j; const LAS float* s = scr + (8 * c) * 33 + n;
;         const unsigned long long o = (unsigned long long)pg8::pk4_fp8(s[0 * 33], s[1 * 33], s[2 * 33], s[3 * 33]) | ((unsigned long long)pg8::pk4_fp8(s[4 * 33], s[5 * 33], s[6 * 33], s[7 * 33]) << 32);
;         *(GAS unsigned long long*)(WT + (size_t)(n0 + n) * K + k0 + 8 * c) = o; }
;     LDS_WAIT(); asm volatile("" ::: "memory");
; }
; __global__ void __launch_bounds__(NWAVES * 64, 2) hybrid_fwd(Args args) {
;     ...
;             if (r < I_O) { if (l >= WO_F8_FROM) p0_transpose_item_f8<true>(args.in[13] + (size_t)l * DM * DM, DM, DM, DM / 32, (unsigned char*)(ws + WS_WO + l * SZ_WO), 64.f, args.in[6] + l * 2048, args.in[12] + l * 2048, 2048, scr, r, lane);
	s_add_i32 s19, s39, 21
	s_min_u32 s19, s19, 31
	s_lshl_b32 s19, s19, 9
	s_add_u32 s12, s22, s19
	s_addc_u32 s13, s23, 0
	global_load_dwordx4 v[100:103], v10, s[12:13]
	s_add_u32 s12, s12, 0x8000
	s_addc_u32 s13, s13, 0
	global_load_dwordx4 v[104:107], v10, s[12:13]
	s_add_u32 s12, s12, 0x8000
	s_addc_u32 s13, s13, 0
	global_load_dwordx4 v[108:111], v10, s[12:13]
	s_add_u32 s12, s12, 0x8000
	s_addc_u32 s13, s13, 0
	global_load_dwordx4 v[112:115], v10, s[12:13]
	s_add_u32 s12, s12, 0x8000
	s_addc_u32 s13, s13, 0
	global_load_dwordx4 v[116:119], v10, s[12:13]
	s_add_u32 s12, s12, 0x8000
	s_addc_u32 s13, s13, 0
	global_load_dwordx4 v[120:123], v10, s[12:13]
	s_add_u32 s12, s12, 0x8000
	s_addc_u32 s13, s13, 0
	global_load_dwordx4 v[124:127], v10, s[12:13]
	s_add_u32 s12, s12, 0x8000
	s_addc_u32 s13, s13, 0
	global_load_dwordx4 v[128:131], v10, s[12:13]
	s_add_i32 s19, s39, 9
	s_min_u32 s19, s19, 31
	s_lshl_b32 s19, s19, 19
	s_add_u32 s14, s50, s19
	s_addc_u32 s15, s51, 0
	ds_read_b32 v170, v6
	ds_read_b32 v171, v6 offset:512
	ds_read_b32 v172, v6 offset:1024
	ds_read_b32 v173, v6 offset:1536
	ds_read_b32 v174, v6 offset:2048
	ds_read_b32 v175, v6 offset:2560
	ds_read_b32 v176, v6 offset:3072
	ds_read_b32 v177, v6 offset:3584
	ds_read_b32 v196, v6 offset:4096
	ds_read_b32 v197, v6 offset:4608
	ds_read_b32 v198, v6 offset:5120
	ds_read_b32 v199, v6 offset:5632
	ds_read_b32 v200, v6 offset:6144
	ds_read_b32 v201, v6 offset:6656
	ds_read_b32 v202, v6 offset:7168
	ds_read_b32 v203, v6 offset:7680
	s_waitcnt lgkmcnt(0)
	v_max_f32_e32 v170, v170, v170
	v_max_f32_e32 v171, v171, v171
	v_max_f32_e32 v172, v172, v172
	v_max_f32_e32 v173, v173, v173
	v_max_f32_e32 v174, v174, v174
	v_max_f32_e32 v175, v175, v175
	v_max_f32_e32 v176, v176, v176
	v_max_f32_e32 v177, v177, v177
	v_max_f32_e32 v196, v196, v196
	v_max_f32_e32 v197, v197, v197
	v_max_f32_e32 v198, v198, v198
	v_max_f32_e32 v199, v199, v199
	v_max_f32_e32 v200, v200, v200
	v_max_f32_e32 v201, v201, v201
	v_max_f32_e32 v202, v202, v202
	v_max_f32_e32 v203, v203, v203
	v_med3_f32 v170, v170, s20, v13
	v_med3_f32 v171, v171, s20, v13
	v_med3_f32 v172, v172, s20, v13
	v_med3_f32 v173, v173, s20, v13
	v_med3_f32 v174, v174, s20, v13
	v_med3_f32 v175, v175, s20, v13
	v_med3_f32 v176, v176, s20, v13
	v_med3_f32 v177, v177, s20, v13
	v_med3_f32 v196, v196, s20, v13
	v_med3_f32 v197, v197, s20, v13
	v_med3_f32 v198, v198, s20, v13
	v_med3_f32 v199, v199, s20, v13
	v_med3_f32 v200, v200, s20, v13
	v_med3_f32 v201, v201, s20, v13
	v_med3_f32 v202, v202, s20, v13
	v_med3_f32 v203, v203, s20, v13
	v_mov_b32_e32 v208, 0
	v_mov_b32_e32 v209, 0
	v_mov_b32_e32 v210, 0
	v_mov_b32_e32 v211, 0
	v_cvt_pk_fp8_f32 v208, v170, v171
	v_cvt_pk_fp8_f32 v209, v174, v175
	v_cvt_pk_fp8_f32 v210, v196, v197
	v_cvt_pk_fp8_f32 v211, v200, v201
	v_cvt_pk_fp8_f32 v208, v172, v173 op_sel:[0,0,1]
	v_cvt_pk_fp8_f32 v209, v176, v177 op_sel:[0,0,1]
	v_cvt_pk_fp8_f32 v210, v198, v199 op_sel:[0,0,1]
	v_cvt_pk_fp8_f32 v211, v202, v203 op_sel:[0,0,1]
	s_nop 0
	global_store_dwordx4 v28, v[208:211], s[14:15]
	ds_read_b32 v170, v8
	ds_read_b32 v171, v8 offset:512
	ds_read_b32 v172, v8 offset:1024
	ds_read_b32 v173, v8 offset:1536
	ds_read_b32 v174, v8 offset:2048
	ds_read_b32 v175, v8 offset:2560
	ds_read_b32 v176, v8 offset:3072
	ds_read_b32 v177, v8 offset:3584
	ds_read_b32 v196, v8 offset:4096
	ds_read_b32 v197, v8 offset:4608
	ds_read_b32 v198, v8 offset:5120
	ds_read_b32 v199, v8 offset:5632
	ds_read_b32 v200, v8 offset:6144
	ds_read_b32 v201, v8 offset:6656
	ds_read_b32 v202, v8 offset:7168
	ds_read_b32 v203, v8 offset:7680
	s_waitcnt lgkmcnt(0)
	v_max_f32_e32 v170, v170, v170
	v_max_f32_e32 v171, v171, v171
	v_max_f32_e32 v172, v172, v172
	v_max_f32_e32 v173, v173, v173
	v_max_f32_e32 v174, v174, v174
	v_max_f32_e32 v175, v175, v175
	v_max_f32_e32 v176, v176, v176
	v_max_f32_e32 v177, v177, v177
	v_max_f32_e32 v196, v196, v196
	v_max_f32_e32 v197, v197, v197
	v_max_f32_e32 v198, v198, v198
	v_max_f32_e32 v199, v199, v199
	v_max_f32_e32 v200, v200, v200
	v_max_f32_e32 v201, v201, v201
	v_max_f32_e32 v202, v202, v202
	v_max_f32_e32 v203, v203, v203
	v_med3_f32 v170, v170, s20, v13
	v_med3_f32 v171, v171, s20, v13
	v_med3_f32 v172, v172, s20, v13
	v_med3_f32 v173, v173, s20, v13
	v_med3_f32 v174, v174, s20, v13
	v_med3_f32 v175, v175, s20, v13
	v_med3_f32 v176, v176, s20, v13
	v_med3_f32 v177, v177, s20, v13
	v_med3_f32 v196, v196, s20, v13
	v_med3_f32 v197, v197, s20, v13
	v_med3_f32 v198, v198, s20, v13
	v_med3_f32 v199, v199, s20, v13
	v_med3_f32 v200, v200, s20, v13
	v_med3_f32 v201, v201, s20, v13
	v_med3_f32 v202, v202, s20, v13
	v_med3_f32 v203, v203, s20, v13
	v_mov_b32_e32 v208, 0
	v_mov_b32_e32 v209, 0
	v_mov_b32_e32 v210, 0
	v_mov_b32_e32 v211, 0
	v_cvt_pk_fp8_f32 v208, v170, v171
	v_cvt_pk_fp8_f32 v209, v174, v175
	v_cvt_pk_fp8_f32 v210, v196, v197
	v_cvt_pk_fp8_f32 v211, v200, v201
	v_cvt_pk_fp8_f32 v208, v172, v173 op_sel:[0,0,1]
	v_cvt_pk_fp8_f32 v209, v176, v177 op_sel:[0,0,1]
	v_cvt_pk_fp8_f32 v210, v198, v199 op_sel:[0,0,1]
	v_cvt_pk_fp8_f32 v211, v202, v203 op_sel:[0,0,1]
	s_nop 0
	global_store_dwordx4 v29, v[208:211], s[14:15]
	s_waitcnt vmcnt(32)
	v_mul_f32_e32 v132, v20, v132
	v_mul_f32_e32 v133, v20, v133
	v_mul_f32_e32 v134, v20, v134
	v_mul_f32_e32 v135, v20, v135
	ds_write_b128 v5, v[132:135]
	v_mul_f32_e32 v136, v21, v136
	v_mul_f32_e32 v137, v21, v137
	v_mul_f32_e32 v138, v21, v138
	v_mul_f32_e32 v139, v21, v139
	ds_write_b128 v5, v[136:139] offset:1024
	v_mul_f32_e32 v140, v22, v140
	v_mul_f32_e32 v141, v22, v141
	v_mul_f32_e32 v142, v22, v142
	v_mul_f32_e32 v143, v22, v143
	ds_write_b128 v5, v[140:143] offset:2048
	v_mul_f32_e32 v144, v23, v144
	v_mul_f32_e32 v145, v23, v145
	v_mul_f32_e32 v146, v23, v146
	v_mul_f32_e32 v147, v23, v147
	ds_write_b128 v5, v[144:147] offset:3072
	v_mul_f32_e32 v148, v24, v148
	v_mul_f32_e32 v149, v24, v149
	v_mul_f32_e32 v150, v24, v150
	v_mul_f32_e32 v151, v24, v151
	ds_write_b128 v5, v[148:151] offset:4096
	v_mul_f32_e32 v152, v25, v152
	v_mul_f32_e32 v153, v25, v153
	v_mul_f32_e32 v154, v25, v154
	v_mul_f32_e32 v155, v25, v155
	ds_write_b128 v5, v[152:155] offset:5120
	v_mul_f32_e32 v156, v26, v156
	v_mul_f32_e32 v157, v26, v157
	v_mul_f32_e32 v158, v26, v158
	v_mul_f32_e32 v159, v26, v159
	ds_write_b128 v5, v[156:159] offset:6144
	v_mul_f32_e32 v160, v27, v160
	v_mul_f32_e32 v161, v27, v161
	v_mul_f32_e32 v162, v27, v162
	v_mul_f32_e32 v163, v27, v163
	ds_write_b128 v5, v[160:163] offset:7168
	s_waitcnt lgkmcnt(0)
	s_barrier
; #define GAS __attribute__((address_space(1)))
; #define LAS __attribute__((address_space(3)))
; #define LDS_WAIT() asm volatile("s_waitcnt lgkmcnt(0)" ::: "memory")
;     const int pr = item >> 1, kb = 2 * (pr / nblk) + (item & 1), nb = pr % nblk, k0 = 64 * kb, n0 = 32 * nb;
;     const int nr = n0 + (lane & 31); const int sc = MAP == 1 ? src_col_in(nr) : nr;
;     float v[32];
; #pragma unroll
;     for (int i = 0; i < 32; ++i) v[i] = sc >= 0 ? W[(size_t)(k0 + 2 * i + (lane >> 5)) * Nsrc + sc] : 0.f;
; #pragma unroll
;     for (int i = 0; i < 32; ++i) { const int k = k0 + 2 * i + (lane >> 5); float x = v[i] * wscale; if (KS) x *= (k < ksplit ? ksA[k] : ksB[k - ksplit]); scr[(2 * i + (lane >> 5)) * 33 + (lane & 31)] = x; }
;     LDS_WAIT(); asm volatile("" ::: "memory");
;     const int c = lane & 7;
; #pragma unroll
;     for (int j = 0; j < 4; ++j) { const int n = (lane >> 3) + 8 * j; const LAS float* s = scr + (8 * c) * 33 + n;
;         const unsigned long long o = (unsigned long long)pg8::pk4_fp8(s[0 * 33], s[1 * 33], s[2 * 33], s[3 * 33]) | ((unsigned long long)pg8::pk4_fp8(s[4 * 33], s[5 * 33], s[6 * 33], s[7 * 33]) << 32);
;         *(GAS unsigned long long*)(WT + (size_t)(n0 + n) * K + k0 + 8 * c) = o; }
;     LDS_WAIT(); asm volatile("" ::: "memory");
; }
; __global__ void __launch_bounds__(NWAVES * 64, 2) hybrid_fwd(Args args) {
;     ...
;             if (r < I_O) { if (l >= WO_F8_FROM) p0_transpose_item_f8<true>(args.in[13] + (size_t)l * DM * DM, DM, DM, DM / 32, (unsigned char*)(ws + WS_WO + l * SZ_WO), 64.f, args.in[6] + l * 2048, args.in[12] + l * 2048, 2048, scr, r, lane);
	s_add_i32 s19, s39, 24
	s_min_u32 s19, s19, 31
	s_lshl_b32 s19, s19, 9
	s_add_u32 s12, s22, s19
	s_addc_u32 s13, s23, 0
	global_load_dwordx4 v[132:135], v10, s[12:13]
	s_add_u32 s12, s12, 0x8000
	s_addc_u32 s13, s13, 0
	global_load_dwordx4 v[136:139], v10, s[12:13]
	s_add_u32 s12, s12, 0x8000
	s_addc_u32 s13, s13, 0
	global_load_dwordx4 v[140:143], v10, s[12:13]
	s_add_u32 s12, s12, 0x8000
	s_addc_u32 s13, s13, 0
	global_load_dwordx4 v[144:147], v10, s[12:13]
	s_add_u32 s12, s12, 0x8000
	s_addc_u32 s13, s13, 0
	global_load_dwordx4 v[148:151], v10, s[12:13]
	s_add_u32 s12, s12, 0x8000
	s_addc_u32 s13, s13, 0
	global_load_dwordx4 v[152:155], v10, s[12:13]
	s_add_u32 s12, s12, 0x8000
	s_addc_u32 s13, s13, 0
	global_load_dwordx4 v[156:159], v10, s[12:13]
	s_add_u32 s12, s12, 0x8000
	s_addc_u32 s13, s13, 0
	global_load_dwordx4 v[160:163], v10, s[12:13]
	s_add_i32 s19, s39, 12
	s_min_u32 s19, s19, 31
	s_lshl_b32 s19, s19, 19
	s_add_u32 s14, s50, s19
	s_addc_u32 s15, s51, 0
	ds_read_b32 v170, v7
	ds_read_b32 v171, v7 offset:512
	ds_read_b32 v172, v7 offset:1024
	ds_read_b32 v173, v7 offset:1536
	ds_read_b32 v174, v7 offset:2048
	ds_read_b32 v175, v7 offset:2560
	ds_read_b32 v176, v7 offset:3072
	ds_read_b32 v177, v7 offset:3584
	ds_read_b32 v196, v7 offset:4096
	ds_read_b32 v197, v7 offset:4608
	ds_read_b32 v198, v7 offset:5120
	ds_read_b32 v199, v7 offset:5632
	ds_read_b32 v200, v7 offset:6144
	ds_read_b32 v201, v7 offset:6656
	ds_read_b32 v202, v7 offset:7168
	ds_read_b32 v203, v7 offset:7680
	s_waitcnt lgkmcnt(0)
	v_max_f32_e32 v170, v170, v170
	v_max_f32_e32 v171, v171, v171
	v_max_f32_e32 v172, v172, v172
	v_max_f32_e32 v173, v173, v173
	v_max_f32_e32 v174, v174, v174
	v_max_f32_e32 v175, v175, v175
	v_max_f32_e32 v176, v176, v176
	v_max_f32_e32 v177, v177, v177
	v_max_f32_e32 v196, v196, v196
	v_max_f32_e32 v197, v197, v197
	v_max_f32_e32 v198, v198, v198
	v_max_f32_e32 v199, v199, v199
	v_max_f32_e32 v200, v200, v200
	v_max_f32_e32 v201, v201, v201
	v_max_f32_e32 v202, v202, v202
	v_max_f32_e32 v203, v203, v203
	v_med3_f32 v170, v170, s20, v13
	v_med3_f32 v171, v171, s20, v13
	v_med3_f32 v172, v172, s20, v13
	v_med3_f32 v173, v173, s20, v13
	v_med3_f32 v174, v174, s20, v13
	v_med3_f32 v175, v175, s20, v13
	v_med3_f32 v176, v176, s20, v13
	v_med3_f32 v177, v177, s20, v13
	v_med3_f32 v196, v196, s20, v13
	v_med3_f32 v197, v197, s20, v13
	v_med3_f32 v198, v198, s20, v13
	v_med3_f32 v199, v199, s20, v13
	v_med3_f32 v200, v200, s20, v13
	v_med3_f32 v201, v201, s20, v13
	v_med3_f32 v202, v202, s20, v13
	v_med3_f32 v203, v203, s20, v13
	v_mov_b32_e32 v208, 0
	v_mov_b32_e32 v209, 0
	v_mov_b32_e32 v210, 0
	v_mov_b32_e32 v211, 0
	v_cvt_pk_fp8_f32 v208, v170, v171
	v_cvt_pk_fp8_f32 v209, v174, v175
	v_cvt_pk_fp8_f32 v210, v196, v197
	v_cvt_pk_fp8_f32 v211, v200, v201
	v_cvt_pk_fp8_f32 v208, v172, v173 op_sel:[0,0,1]
	v_cvt_pk_fp8_f32 v209, v176, v177 op_sel:[0,0,1]
	v_cvt_pk_fp8_f32 v210, v198, v199 op_sel:[0,0,1]
	v_cvt_pk_fp8_f32 v211, v202, v203 op_sel:[0,0,1]
	s_nop 0
	global_store_dwordx4 v28, v[208:211], s[14:15]
	ds_read_b32 v170, v9
	ds_read_b32 v171, v9 offset:512
	ds_read_b32 v172, v9 offset:1024
	ds_read_b32 v173, v9 offset:1536
	ds_read_b32 v174, v9 offset:2048
	ds_read_b32 v175, v9 offset:2560
	ds_read_b32 v176, v9 offset:3072
	ds_read_b32 v177, v9 offset:3584
	ds_read_b32 v196, v9 offset:4096
	ds_read_b32 v197, v9 offset:4608
	ds_read_b32 v198, v9 offset:5120
	ds_read_b32 v199, v9 offset:5632
	ds_read_b32 v200, v9 offset:6144
	ds_read_b32 v201, v9 offset:6656
	ds_read_b32 v202, v9 offset:7168
	ds_read_b32 v203, v9 offset:7680
	s_waitcnt lgkmcnt(0)
	v_max_f32_e32 v170, v170, v170
	v_max_f32_e32 v171, v171, v171
	v_max_f32_e32 v172, v172, v172
	v_max_f32_e32 v173, v173, v173
	v_max_f32_e32 v174, v174, v174
	v_max_f32_e32 v175, v175, v175
	v_max_f32_e32 v176, v176, v176
	v_max_f32_e32 v177, v177, v177
	v_max_f32_e32 v196, v196, v196
	v_max_f32_e32 v197, v197, v197
	v_max_f32_e32 v198, v198, v198
	v_max_f32_e32 v199, v199, v199
	v_max_f32_e32 v200, v200, v200
	v_max_f32_e32 v201, v201, v201
	v_max_f32_e32 v202, v202, v202
	v_max_f32_e32 v203, v203, v203
	v_med3_f32 v170, v170, s20, v13
	v_med3_f32 v171, v171, s20, v13
	v_med3_f32 v172, v172, s20, v13
	v_med3_f32 v173, v173, s20, v13
	v_med3_f32 v174, v174, s20, v13
	v_med3_f32 v175, v175, s20, v13
	v_med3_f32 v176, v176, s20, v13
	v_med3_f32 v177, v177, s20, v13
	v_med3_f32 v196, v196, s20, v13
	v_med3_f32 v197, v197, s20, v13
	v_med3_f32 v198, v198, s20, v13
	v_med3_f32 v199, v199, s20, v13
	v_med3_f32 v200, v200, s20, v13
	v_med3_f32 v201, v201, s20, v13
	v_med3_f32 v202, v202, s20, v13
	v_med3_f32 v203, v203, s20, v13
	v_mov_b32_e32 v208, 0
	v_mov_b32_e32 v209, 0
	v_mov_b32_e32 v210, 0
	v_mov_b32_e32 v211, 0
	v_cvt_pk_fp8_f32 v208, v170, v171
	v_cvt_pk_fp8_f32 v209, v174, v175
	v_cvt_pk_fp8_f32 v210, v196, v197
	v_cvt_pk_fp8_f32 v211, v200, v201
	v_cvt_pk_fp8_f32 v208, v172, v173 op_sel:[0,0,1]
	v_cvt_pk_fp8_f32 v209, v176, v177 op_sel:[0,0,1]
	v_cvt_pk_fp8_f32 v210, v198, v199 op_sel:[0,0,1]
	v_cvt_pk_fp8_f32 v211, v202, v203 op_sel:[0,0,1]
	s_nop 0
	global_store_dwordx4 v29, v[208:211], s[14:15]
	s_waitcnt vmcnt(32)
	v_mul_f32_e32 v36, v20, v36
	v_mul_f32_e32 v37, v20, v37
	v_mul_f32_e32 v38, v20, v38
	v_mul_f32_e32 v39, v20, v39
	ds_write_b128 v4, v[36:39]
	v_mul_f32_e32 v40, v21, v40
	v_mul_f32_e32 v41, v21, v41
	v_mul_f32_e32 v42, v21, v42
	v_mul_f32_e32 v43, v21, v43
	ds_write_b128 v4, v[40:43] offset:1024
	v_mul_f32_e32 v44, v22, v44
	v_mul_f32_e32 v45, v22, v45
	v_mul_f32_e32 v46, v22, v46
	v_mul_f32_e32 v47, v22, v47
	ds_write_b128 v4, v[44:47] offset:2048
	v_mul_f32_e32 v48, v23, v48
	v_mul_f32_e32 v49, v23, v49
	v_mul_f32_e32 v50, v23, v50
	v_mul_f32_e32 v51, v23, v51
	ds_write_b128 v4, v[48:51] offset:3072
	v_mul_f32_e32 v52, v24, v52
	v_mul_f32_e32 v53, v24, v53
	v_mul_f32_e32 v54, v24, v54
	v_mul_f32_e32 v55, v24, v55
	ds_write_b128 v4, v[52:55] offset:4096
	v_mul_f32_e32 v56, v25, v56
	v_mul_f32_e32 v57, v25, v57
	v_mul_f32_e32 v58, v25, v58
	v_mul_f32_e32 v59, v25, v59
	ds_write_b128 v4, v[56:59] offset:5120
	v_mul_f32_e32 v60, v26, v60
	v_mul_f32_e32 v61, v26, v61
	v_mul_f32_e32 v62, v26, v62
	v_mul_f32_e32 v63, v26, v63
	ds_write_b128 v4, v[60:63] offset:6144
	v_mul_f32_e32 v64, v27, v64
	v_mul_f32_e32 v65, v27, v65
	v_mul_f32_e32 v66, v27, v66
	v_mul_f32_e32 v67, v27, v67
	ds_write_b128 v4, v[64:67] offset:7168
	s_waitcnt lgkmcnt(0)
	s_barrier
; #define GAS __attribute__((address_space(1)))
; #define LAS __attribute__((address_space(3)))
; #define LDS_WAIT() asm volatile("s_waitcnt lgkmcnt(0)" ::: "memory")
;     const int pr = item >> 1, kb = 2 * (pr / nblk) + (item & 1), nb = pr % nblk, k0 = 64 * kb, n0 = 32 * nb;
;     const int nr = n0 + (lane & 31); const int sc = MAP == 1 ? src_col_in(nr) : nr;
;     float v[32];
; #pragma unroll
;     for (int i = 0; i < 32; ++i) v[i] = sc >= 0 ? W[(size_t)(k0 + 2 * i + (lane >> 5)) * Nsrc + sc] : 0.f;
; #pragma unroll
;     for (int i = 0; i < 32; ++i) { const int k = k0 + 2 * i + (lane >> 5); float x = v[i] * wscale; if (KS) x *= (k < ksplit ? ksA[k] : ksB[k - ksplit]); scr[(2 * i + (lane >> 5)) * 33 + (lane & 31)] = x; }
;     LDS_WAIT(); asm volatile("" ::: "memory");
;     const int c = lane & 7;
; #pragma unroll
;     for (int j = 0; j < 4; ++j) { const int n = (lane >> 3) + 8 * j; const LAS float* s = scr + (8 * c) * 33 + n;
;         const unsigned long long o = (unsigned long long)pg8::pk4_fp8(s[0 * 33], s[1 * 33], s[2 * 33], s[3 * 33]) | ((unsigned long long)pg8::pk4_fp8(s[4 * 33], s[5 * 33], s[6 * 33], s[7 * 33]) << 32);
;         *(GAS unsigned long long*)(WT + (size_t)(n0 + n) * K + k0 + 8 * c) = o; }
;     LDS_WAIT(); asm volatile("" ::: "memory");
; }
; __global__ void __launch_bounds__(NWAVES * 64, 2) hybrid_fwd(Args args) {
;     ...
;             if (r < I_O) { if (l >= WO_F8_FROM) p0_transpose_item_f8<true>(args.in[13] + (size_t)l * DM * DM, DM, DM, DM / 32, (unsigned char*)(ws + WS_WO + l * SZ_WO), 64.f, args.in[6] + l * 2048, args.in[12] + l * 2048, 2048, scr, r, lane);
	s_add_i32 s19, s39, 27
	s_min_u32 s19, s19, 31
	s_lshl_b32 s19, s19, 9
	s_add_u32 s12, s22, s19
	s_addc_u32 s13, s23, 0
	global_load_dwordx4 v[36:39], v10, s[12:13]
	s_add_u32 s12, s12, 0x8000
	s_addc_u32 s13, s13, 0
	global_load_dwordx4 v[40:43], v10, s[12:13]
	s_add_u32 s12, s12, 0x8000
	s_addc_u32 s13, s13, 0
	global_load_dwordx4 v[44:47], v10, s[12:13]
	s_add_u32 s12, s12, 0x8000
	s_addc_u32 s13, s13, 0
	global_load_dwordx4 v[48:51], v10, s[12:13]
	s_add_u32 s12, s12, 0x8000
	s_addc_u32 s13, s13, 0
	global_load_dwordx4 v[52:55], v10, s[12:13]
	s_add_u32 s12, s12, 0x8000
	s_addc_u32 s13, s13, 0
	global_load_dwordx4 v[56:59], v10, s[12:13]
	s_add_u32 s12, s12, 0x8000
	s_addc_u32 s13, s13, 0
	global_load_dwordx4 v[60:63], v10, s[12:13]
	s_add_u32 s12, s12, 0x8000
	s_addc_u32 s13, s13, 0
	global_load_dwordx4 v[64:67], v10, s[12:13]
	s_add_i32 s19, s39, 15
	s_min_u32 s19, s19, 31
	s_lshl_b32 s19, s19, 19
	s_add_u32 s14, s50, s19
	s_addc_u32 s15, s51, 0
	ds_read_b32 v170, v6
	ds_read_b32 v171, v6 offset:512
	ds_read_b32 v172, v6 offset:1024
	ds_read_b32 v173, v6 offset:1536
	ds_read_b32 v174, v6 offset:2048
	ds_read_b32 v175, v6 offset:2560
	ds_read_b32 v176, v6 offset:3072
	ds_read_b32 v177, v6 offset:3584
	ds_read_b32 v196, v6 offset:4096
	ds_read_b32 v197, v6 offset:4608
	ds_read_b32 v198, v6 offset:5120
	ds_read_b32 v199, v6 offset:5632
	ds_read_b32 v200, v6 offset:6144
	ds_read_b32 v201, v6 offset:6656
	ds_read_b32 v202, v6 offset:7168
	ds_read_b32 v203, v6 offset:7680
	s_waitcnt lgkmcnt(0)
	v_max_f32_e32 v170, v170, v170
	v_max_f32_e32 v171, v171, v171
	v_max_f32_e32 v172, v172, v172
	v_max_f32_e32 v173, v173, v173
	v_max_f32_e32 v174, v174, v174
	v_max_f32_e32 v175, v175, v175
	v_max_f32_e32 v176, v176, v176
	v_max_f32_e32 v177, v177, v177
	v_max_f32_e32 v196, v196, v196
	v_max_f32_e32 v197, v197, v197
	v_max_f32_e32 v198, v198, v198
	v_max_f32_e32 v199, v199, v199
	v_max_f32_e32 v200, v200, v200
	v_max_f32_e32 v201, v201, v201
	v_max_f32_e32 v202, v202, v202
	v_max_f32_e32 v203, v203, v203
	v_med3_f32 v170, v170, s20, v13
	v_med3_f32 v171, v171, s20, v13
	v_med3_f32 v172, v172, s20, v13
	v_med3_f32 v173, v173, s20, v13
	v_med3_f32 v174, v174, s20, v13
	v_med3_f32 v175, v175, s20, v13
	v_med3_f32 v176, v176, s20, v13
	v_med3_f32 v177, v177, s20, v13
	v_med3_f32 v196, v196, s20, v13
	v_med3_f32 v197, v197, s20, v13
	v_med3_f32 v198, v198, s20, v13
	v_med3_f32 v199, v199, s20, v13
	v_med3_f32 v200, v200, s20, v13
	v_med3_f32 v201, v201, s20, v13
	v_med3_f32 v202, v202, s20, v13
	v_med3_f32 v203, v203, s20, v13
	v_mov_b32_e32 v208, 0
	v_mov_b32_e32 v209, 0
	v_mov_b32_e32 v210, 0
	v_mov_b32_e32 v211, 0
	v_cvt_pk_fp8_f32 v208, v170, v171
	v_cvt_pk_fp8_f32 v209, v174, v175
	v_cvt_pk_fp8_f32 v210, v196, v197
	v_cvt_pk_fp8_f32 v211, v200, v201
	v_cvt_pk_fp8_f32 v208, v172, v173 op_sel:[0,0,1]
	v_cvt_pk_fp8_f32 v209, v176, v177 op_sel:[0,0,1]
	v_cvt_pk_fp8_f32 v210, v198, v199 op_sel:[0,0,1]
	v_cvt_pk_fp8_f32 v211, v202, v203 op_sel:[0,0,1]
	s_nop 0
	global_store_dwordx4 v28, v[208:211], s[14:15]
	ds_read_b32 v170, v8
	ds_read_b32 v171, v8 offset:512
	ds_read_b32 v172, v8 offset:1024
	ds_read_b32 v173, v8 offset:1536
	ds_read_b32 v174, v8 offset:2048
	ds_read_b32 v175, v8 offset:2560
	ds_read_b32 v176, v8 offset:3072
	ds_read_b32 v177, v8 offset:3584
	ds_read_b32 v196, v8 offset:4096
	ds_read_b32 v197, v8 offset:4608
	ds_read_b32 v198, v8 offset:5120
	ds_read_b32 v199, v8 offset:5632
	ds_read_b32 v200, v8 offset:6144
	ds_read_b32 v201, v8 offset:6656
	ds_read_b32 v202, v8 offset:7168
	ds_read_b32 v203, v8 offset:7680
	s_waitcnt lgkmcnt(0)
	v_max_f32_e32 v170, v170, v170
	v_max_f32_e32 v171, v171, v171
	v_max_f32_e32 v172, v172, v172
	v_max_f32_e32 v173, v173, v173
	v_max_f32_e32 v174, v174, v174
	v_max_f32_e32 v175, v175, v175
	v_max_f32_e32 v176, v176, v176
	v_max_f32_e32 v177, v177, v177
	v_max_f32_e32 v196, v196, v196
	v_max_f32_e32 v197, v197, v197
	v_max_f32_e32 v198, v198, v198
	v_max_f32_e32 v199, v199, v199
	v_max_f32_e32 v200, v200, v200
	v_max_f32_e32 v201, v201, v201
	v_max_f32_e32 v202, v202, v202
	v_max_f32_e32 v203, v203, v203
	v_med3_f32 v170, v170, s20, v13
	v_med3_f32 v171, v171, s20, v13
	v_med3_f32 v172, v172, s20, v13
	v_med3_f32 v173, v173, s20, v13
	v_med3_f32 v174, v174, s20, v13
	v_med3_f32 v175, v175, s20, v13
	v_med3_f32 v176, v176, s20, v13
	v_med3_f32 v177, v177, s20, v13
	v_med3_f32 v196, v196, s20, v13
	v_med3_f32 v197, v197, s20, v13
	v_med3_f32 v198, v198, s20, v13
	v_med3_f32 v199, v199, s20, v13
	v_med3_f32 v200, v200, s20, v13
	v_med3_f32 v201, v201, s20, v13
	v_med3_f32 v202, v202, s20, v13
	v_med3_f32 v203, v203, s20, v13
	v_mov_b32_e32 v208, 0
	v_mov_b32_e32 v209, 0
	v_mov_b32_e32 v210, 0
	v_mov_b32_e32 v211, 0
	v_cvt_pk_fp8_f32 v208, v170, v171
	v_cvt_pk_fp8_f32 v209, v174, v175
	v_cvt_pk_fp8_f32 v210, v196, v197
	v_cvt_pk_fp8_f32 v211, v200, v201
	v_cvt_pk_fp8_f32 v208, v172, v173 op_sel:[0,0,1]
	v_cvt_pk_fp8_f32 v209, v176, v177 op_sel:[0,0,1]
	v_cvt_pk_fp8_f32 v210, v198, v199 op_sel:[0,0,1]
	v_cvt_pk_fp8_f32 v211, v202, v203 op_sel:[0,0,1]
	s_nop 0
	global_store_dwordx4 v29, v[208:211], s[14:15]
	s_waitcnt vmcnt(32)
	v_mul_f32_e32 v68, v20, v68
	v_mul_f32_e32 v69, v20, v69
	v_mul_f32_e32 v70, v20, v70
	v_mul_f32_e32 v71, v20, v71
	ds_write_b128 v5, v[68:71]
	v_mul_f32_e32 v72, v21, v72
	v_mul_f32_e32 v73, v21, v73
	v_mul_f32_e32 v74, v21, v74
	v_mul_f32_e32 v75, v21, v75
	ds_write_b128 v5, v[72:75] offset:1024
	v_mul_f32_e32 v76, v22, v76
	v_mul_f32_e32 v77, v22, v77
	v_mul_f32_e32 v78, v22, v78
	v_mul_f32_e32 v79, v22, v79
	ds_write_b128 v5, v[76:79] offset:2048
	v_mul_f32_e32 v80, v23, v80
	v_mul_f32_e32 v81, v23, v81
	v_mul_f32_e32 v82, v23, v82
	v_mul_f32_e32 v83, v23, v83
	ds_write_b128 v5, v[80:83] offset:3072
	v_mul_f32_e32 v84, v24, v84
	v_mul_f32_e32 v85, v24, v85
	v_mul_f32_e32 v86, v24, v86
	v_mul_f32_e32 v87, v24, v87
	ds_write_b128 v5, v[84:87] offset:4096
	v_mul_f32_e32 v88, v25, v88
	v_mul_f32_e32 v89, v25, v89
	v_mul_f32_e32 v90, v25, v90
	v_mul_f32_e32 v91, v25, v91
	ds_write_b128 v5, v[88:91] offset:5120
	v_mul_f32_e32 v92, v26, v92
	v_mul_f32_e32 v93, v26, v93
	v_mul_f32_e32 v94, v26, v94
	v_mul_f32_e32 v95, v26, v95
	ds_write_b128 v5, v[92:95] offset:6144
	v_mul_f32_e32 v96, v27, v96
	v_mul_f32_e32 v97, v27, v97
	v_mul_f32_e32 v98, v27, v98
	v_mul_f32_e32 v99, v27, v99
	ds_write_b128 v5, v[96:99] offset:7168
	s_waitcnt lgkmcnt(0)
	s_barrier
; #define GAS __attribute__((address_space(1)))
; #define LAS __attribute__((address_space(3)))
; #define LDS_WAIT() asm volatile("s_waitcnt lgkmcnt(0)" ::: "memory")
;     const int pr = item >> 1, kb = 2 * (pr / nblk) + (item & 1), nb = pr % nblk, k0 = 64 * kb, n0 = 32 * nb;
;     const int nr = n0 + (lane & 31); const int sc = MAP == 1 ? src_col_in(nr) : nr;
;     float v[32];
; #pragma unroll
;     for (int i = 0; i < 32; ++i) v[i] = sc >= 0 ? W[(size_t)(k0 + 2 * i + (lane >> 5)) * Nsrc + sc] : 0.f;
; #pragma unroll
;     for (int i = 0; i < 32; ++i) { const int k = k0 + 2 * i + (lane >> 5); float x = v[i] * wscale; if (KS) x *= (k < ksplit ? ksA[k] : ksB[k - ksplit]); scr[(2 * i + (lane >> 5)) * 33 + (lane & 31)] = x; }
;     LDS_WAIT(); asm volatile("" ::: "memory");
;     const int c = lane & 7;
; #pragma unroll
;     for (int j = 0; j < 4; ++j) { const int n = (lane >> 3) + 8 * j; const LAS float* s = scr + (8 * c) * 33 + n;
;         const unsigned long long o = (unsigned long long)pg8::pk4_fp8(s[0 * 33], s[1 * 33], s[2 * 33], s[3 * 33]) | ((unsigned long long)pg8::pk4_fp8(s[4 * 33], s[5 * 33], s[6 * 33], s[7 * 33]) << 32);
;         *(GAS unsigned long long*)(WT + (size_t)(n0 + n) * K + k0 + 8 * c) = o; }
;     LDS_WAIT(); asm volatile("" ::: "memory");
; }
; __global__ void __launch_bounds__(NWAVES * 64, 2) hybrid_fwd(Args args) {
;     ...
;             if (r < I_O) { if (l >= WO_F8_FROM) p0_transpose_item_f8<true>(args.in[13] + (size_t)l * DM * DM, DM, DM, DM / 32, (unsigned char*)(ws + WS_WO + l * SZ_WO), 64.f, args.in[6] + l * 2048, args.in[12] + l * 2048, 2048, scr, r, lane);
	s_add_i32 s19, s39, 30
	s_min_u32 s19, s19, 31
	s_lshl_b32 s19, s19, 9
	s_add_u32 s12, s22, s19
	s_addc_u32 s13, s23, 0
	global_load_dwordx4 v[68:71], v10, s[12:13]
	s_add_u32 s12, s12, 0x8000
	s_addc_u32 s13, s13, 0
	global_load_dwordx4 v[72:75], v10, s[12:13]
	s_add_u32 s12, s12, 0x8000
	s_addc_u32 s13, s13, 0
	global_load_dwordx4 v[76:79], v10, s[12:13]
	s_add_u32 s12, s12, 0x8000
	s_addc_u32 s13, s13, 0
	global_load_dwordx4 v[80:83], v10, s[12:13]
	s_add_u32 s12, s12, 0x8000
	s_addc_u32 s13, s13, 0
	global_load_dwordx4 v[84:87], v10, s[12:13]
	s_add_u32 s12, s12, 0x8000
	s_addc_u32 s13, s13, 0
	global_load_dwordx4 v[88:91], v10, s[12:13]
	s_add_u32 s12, s12, 0x8000
	s_addc_u32 s13, s13, 0
	global_load_dwordx4 v[92:95], v10, s[12:13]
	s_add_u32 s12, s12, 0x8000
	s_addc_u32 s13, s13, 0
	global_load_dwordx4 v[96:99], v10, s[12:13]
	s_add_i32 s19, s39, 18
	s_min_u32 s19, s19, 31
	s_lshl_b32 s19, s19, 19
	s_add_u32 s14, s50, s19
	s_addc_u32 s15, s51, 0
	ds_read_b32 v170, v7
	ds_read_b32 v171, v7 offset:512
	ds_read_b32 v172, v7 offset:1024
	ds_read_b32 v173, v7 offset:1536
	ds_read_b32 v174, v7 offset:2048
	ds_read_b32 v175, v7 offset:2560
	ds_read_b32 v176, v7 offset:3072
	ds_read_b32 v177, v7 offset:3584
	ds_read_b32 v196, v7 offset:4096
	ds_read_b32 v197, v7 offset:4608
	ds_read_b32 v198, v7 offset:5120
	ds_read_b32 v199, v7 offset:5632
	ds_read_b32 v200, v7 offset:6144
	ds_read_b32 v201, v7 offset:6656
	ds_read_b32 v202, v7 offset:7168
	ds_read_b32 v203, v7 offset:7680
	s_waitcnt lgkmcnt(0)
	v_max_f32_e32 v170, v170, v170
	v_max_f32_e32 v171, v171, v171
	v_max_f32_e32 v172, v172, v172
	v_max_f32_e32 v173, v173, v173
	v_max_f32_e32 v174, v174, v174
	v_max_f32_e32 v175, v175, v175
	v_max_f32_e32 v176, v176, v176
	v_max_f32_e32 v177, v177, v177
	v_max_f32_e32 v196, v196, v196
	v_max_f32_e32 v197, v197, v197
	v_max_f32_e32 v198, v198, v198
	v_max_f32_e32 v199, v199, v199
	v_max_f32_e32 v200, v200, v200
	v_max_f32_e32 v201, v201, v201
	v_max_f32_e32 v202, v202, v202
	v_max_f32_e32 v203, v203, v203
	v_med3_f32 v170, v170, s20, v13
	v_med3_f32 v171, v171, s20, v13
	v_med3_f32 v172, v172, s20, v13
	v_med3_f32 v173, v173, s20, v13
	v_med3_f32 v174, v174, s20, v13
	v_med3_f32 v175, v175, s20, v13
	v_med3_f32 v176, v176, s20, v13
	v_med3_f32 v177, v177, s20, v13
	v_med3_f32 v196, v196, s20, v13
	v_med3_f32 v197, v197, s20, v13
	v_med3_f32 v198, v198, s20, v13
	v_med3_f32 v199, v199, s20, v13
	v_med3_f32 v200, v200, s20, v13
	v_med3_f32 v201, v201, s20, v13
	v_med3_f32 v202, v202, s20, v13
	v_med3_f32 v203, v203, s20, v13
	v_mov_b32_e32 v208, 0
	v_mov_b32_e32 v209, 0
	v_mov_b32_e32 v210, 0
	v_mov_b32_e32 v211, 0
	v_cvt_pk_fp8_f32 v208, v170, v171
	v_cvt_pk_fp8_f32 v209, v174, v175
	v_cvt_pk_fp8_f32 v210, v196, v197
	v_cvt_pk_fp8_f32 v211, v200, v201
	v_cvt_pk_fp8_f32 v208, v172, v173 op_sel:[0,0,1]
	v_cvt_pk_fp8_f32 v209, v176, v177 op_sel:[0,0,1]
	v_cvt_pk_fp8_f32 v210, v198, v199 op_sel:[0,0,1]
	v_cvt_pk_fp8_f32 v211, v202, v203 op_sel:[0,0,1]
	s_nop 0
	global_store_dwordx4 v28, v[208:211], s[14:15]
	ds_read_b32 v170, v9
	ds_read_b32 v171, v9 offset:512
	ds_read_b32 v172, v9 offset:1024
	ds_read_b32 v173, v9 offset:1536
	ds_read_b32 v174, v9 offset:2048
	ds_read_b32 v175, v9 offset:2560
	ds_read_b32 v176, v9 offset:3072
	ds_read_b32 v177, v9 offset:3584
	ds_read_b32 v196, v9 offset:4096
	ds_read_b32 v197, v9 offset:4608
	ds_read_b32 v198, v9 offset:5120
	ds_read_b32 v199, v9 offset:5632
	ds_read_b32 v200, v9 offset:6144
	ds_read_b32 v201, v9 offset:6656
	ds_read_b32 v202, v9 offset:7168
	ds_read_b32 v203, v9 offset:7680
	s_waitcnt lgkmcnt(0)
	v_max_f32_e32 v170, v170, v170
	v_max_f32_e32 v171, v171, v171
	v_max_f32_e32 v172, v172, v172
	v_max_f32_e32 v173, v173, v173
	v_max_f32_e32 v174, v174, v174
	v_max_f32_e32 v175, v175, v175
	v_max_f32_e32 v176, v176, v176
	v_max_f32_e32 v177, v177, v177
	v_max_f32_e32 v196, v196, v196
	v_max_f32_e32 v197, v197, v197
	v_max_f32_e32 v198, v198, v198
	v_max_f32_e32 v199, v199, v199
	v_max_f32_e32 v200, v200, v200
	v_max_f32_e32 v201, v201, v201
	v_max_f32_e32 v202, v202, v202
	v_max_f32_e32 v203, v203, v203
	v_med3_f32 v170, v170, s20, v13
	v_med3_f32 v171, v171, s20, v13
	v_med3_f32 v172, v172, s20, v13
	v_med3_f32 v173, v173, s20, v13
	v_med3_f32 v174, v174, s20, v13
	v_med3_f32 v175, v175, s20, v13
	v_med3_f32 v176, v176, s20, v13
	v_med3_f32 v177, v177, s20, v13
	v_med3_f32 v196, v196, s20, v13
	v_med3_f32 v197, v197, s20, v13
	v_med3_f32 v198, v198, s20, v13
	v_med3_f32 v199, v199, s20, v13
	v_med3_f32 v200, v200, s20, v13
	v_med3_f32 v201, v201, s20, v13
	v_med3_f32 v202, v202, s20, v13
	v_med3_f32 v203, v203, s20, v13
	v_mov_b32_e32 v208, 0
	v_mov_b32_e32 v209, 0
	v_mov_b32_e32 v210, 0
	v_mov_b32_e32 v211, 0
	v_cvt_pk_fp8_f32 v208, v170, v171
	v_cvt_pk_fp8_f32 v209, v174, v175
	v_cvt_pk_fp8_f32 v210, v196, v197
	v_cvt_pk_fp8_f32 v211, v200, v201
	v_cvt_pk_fp8_f32 v208, v172, v173 op_sel:[0,0,1]
	v_cvt_pk_fp8_f32 v209, v176, v177 op_sel:[0,0,1]
	v_cvt_pk_fp8_f32 v210, v198, v199 op_sel:[0,0,1]
	v_cvt_pk_fp8_f32 v211, v202, v203 op_sel:[0,0,1]
	s_nop 0
	global_store_dwordx4 v29, v[208:211], s[14:15]
	s_waitcnt vmcnt(32)
	v_mul_f32_e32 v100, v20, v100
	v_mul_f32_e32 v101, v20, v101
	v_mul_f32_e32 v102, v20, v102
	v_mul_f32_e32 v103, v20, v103
	ds_write_b128 v4, v[100:103]
	v_mul_f32_e32 v104, v21, v104
	v_mul_f32_e32 v105, v21, v105
	v_mul_f32_e32 v106, v21, v106
	v_mul_f32_e32 v107, v21, v107
	ds_write_b128 v4, v[104:107] offset:1024
	v_mul_f32_e32 v108, v22, v108
	v_mul_f32_e32 v109, v22, v109
	v_mul_f32_e32 v110, v22, v110
	v_mul_f32_e32 v111, v22, v111
	ds_write_b128 v4, v[108:111] offset:2048
	v_mul_f32_e32 v112, v23, v112
	v_mul_f32_e32 v113, v23, v113
	v_mul_f32_e32 v114, v23, v114
	v_mul_f32_e32 v115, v23, v115
	ds_write_b128 v4, v[112:115] offset:3072
	v_mul_f32_e32 v116, v24, v116
	v_mul_f32_e32 v117, v24, v117
	v_mul_f32_e32 v118, v24, v118
	v_mul_f32_e32 v119, v24, v119
	ds_write_b128 v4, v[116:119] offset:4096
	v_mul_f32_e32 v120, v25, v120
	v_mul_f32_e32 v121, v25, v121
	v_mul_f32_e32 v122, v25, v122
	v_mul_f32_e32 v123, v25, v123
	ds_write_b128 v4, v[120:123] offset:5120
	v_mul_f32_e32 v124, v26, v124
	v_mul_f32_e32 v125, v26, v125
	v_mul_f32_e32 v126, v26, v126
	v_mul_f32_e32 v127, v26, v127
	ds_write_b128 v4, v[124:127] offset:6144
	v_mul_f32_e32 v128, v27, v128
	v_mul_f32_e32 v129, v27, v129
	v_mul_f32_e32 v130, v27, v130
	v_mul_f32_e32 v131, v27, v131
	ds_write_b128 v4, v[128:131] offset:7168
	s_waitcnt lgkmcnt(0)
	s_barrier
; #define GAS __attribute__((address_space(1)))
; #define LAS __attribute__((address_space(3)))
; #define LDS_WAIT() asm volatile("s_waitcnt lgkmcnt(0)" ::: "memory")
;     const int pr = item >> 1, kb = 2 * (pr / nblk) + (item & 1), nb = pr % nblk, k0 = 64 * kb, n0 = 32 * nb;
;     const int nr = n0 + (lane & 31); const int sc = MAP == 1 ? src_col_in(nr) : nr;
;     float v[32];
; #pragma unroll
;     for (int i = 0; i < 32; ++i) v[i] = sc >= 0 ? W[(size_t)(k0 + 2 * i + (lane >> 5)) * Nsrc + sc] : 0.f;
; #pragma unroll
;     for (int i = 0; i < 32; ++i) { const int k = k0 + 2 * i + (lane >> 5); float x = v[i] * wscale; if (KS) x *= (k < ksplit ? ksA[k] : ksB[k - ksplit]); scr[(2 * i + (lane >> 5)) * 33 + (lane & 31)] = x; }
;     LDS_WAIT(); asm volatile("" ::: "memory");
;     const int c = lane & 7;
; #pragma unroll
;     for (int j = 0; j < 4; ++j) { const int n = (lane >> 3) + 8 * j; const LAS float* s = scr + (8 * c) * 33 + n;
;         const unsigned long long o = (unsigned long long)pg8::pk4_fp8(s[0 * 33], s[1 * 33], s[2 * 33], s[3 * 33]) | ((unsigned long long)pg8::pk4_fp8(s[4 * 33], s[5 * 33], s[6 * 33], s[7 * 33]) << 32);
;         *(GAS unsigned long long*)(WT + (size_t)(n0 + n) * K + k0 + 8 * c) = o; }
;     LDS_WAIT(); asm volatile("" ::: "memory");
; }
; __global__ void __launch_bounds__(NWAVES * 64, 2) hybrid_fwd(Args args) {
;     ...
;             if (r < I_UP) { p0_transpose_item_f8<true>(args.in[15] + (size_t)l * DM * FF, DM, FF, FF / 32, (unsigned char*)(ws + WS_WUP + l * SZ_WUP), WUP8_SCALE, args.in[14] + l * DM, args.in[14] + l * DM, DM, scr, r, lane); continue; } r -= I_UP;
	s_add_i32 s19, s39, 96
	s_min_u32 s19, s19, 127
	s_lshl_b32 s19, s19, 9
	s_add_u32 s12, s46, s19
	s_addc_u32 s13, s47, 0
	global_load_dwordx4 v[100:103], v30, s[12:13]
	s_add_u32 s12, s12, 0x20000
	s_addc_u32 s13, s13, 0
	global_load_dwordx4 v[104:107], v30, s[12:13]
	s_add_u32 s12, s12, 0x20000
	s_addc_u32 s13, s13, 0
	global_load_dwordx4 v[108:111], v30, s[12:13]
	s_add_u32 s12, s12, 0x20000
	s_addc_u32 s13, s13, 0
	global_load_dwordx4 v[112:115], v30, s[12:13]
	s_add_u32 s12, s12, 0x20000
	s_addc_u32 s13, s13, 0
	global_load_dwordx4 v[116:119], v30, s[12:13]
	s_add_u32 s12, s12, 0x20000
	s_addc_u32 s13, s13, 0
	global_load_dwordx4 v[120:123], v30, s[12:13]
	s_add_u32 s12, s12, 0x20000
	s_addc_u32 s13, s13, 0
	global_load_dwordx4 v[124:127], v30, s[12:13]
	s_add_u32 s12, s12, 0x20000
	s_addc_u32 s13, s13, 0
	global_load_dwordx4 v[128:131], v30, s[12:13]
	s_add_i32 s19, s39, 21
	s_min_u32 s19, s19, 31
	s_lshl_b32 s19, s19, 19
	s_add_u32 s14, s50, s19
	s_addc_u32 s15, s51, 0
	ds_read_b32 v170, v6
	ds_read_b32 v171, v6 offset:512
	ds_read_b32 v172, v6 offset:1024
	ds_read_b32 v173, v6 offset:1536
	ds_read_b32 v174, v6 offset:2048
	ds_read_b32 v175, v6 offset:2560
	ds_read_b32 v176, v6 offset:3072
	ds_read_b32 v177, v6 offset:3584
	ds_read_b32 v196, v6 offset:4096
	ds_read_b32 v197, v6 offset:4608
	ds_read_b32 v198, v6 offset:5120
	ds_read_b32 v199, v6 offset:5632
	ds_read_b32 v200, v6 offset:6144
	ds_read_b32 v201, v6 offset:6656
	ds_read_b32 v202, v6 offset:7168
	ds_read_b32 v203, v6 offset:7680
	s_waitcnt lgkmcnt(0)
	v_max_f32_e32 v170, v170, v170
	v_max_f32_e32 v171, v171, v171
	v_max_f32_e32 v172, v172, v172
	v_max_f32_e32 v173, v173, v173
	v_max_f32_e32 v174, v174, v174
	v_max_f32_e32 v175, v175, v175
	v_max_f32_e32 v176, v176, v176
	v_max_f32_e32 v177, v177, v177
	v_max_f32_e32 v196, v196, v196
	v_max_f32_e32 v197, v197, v197
	v_max_f32_e32 v198, v198, v198
	v_max_f32_e32 v199, v199, v199
	v_max_f32_e32 v200, v200, v200
	v_max_f32_e32 v201, v201, v201
	v_max_f32_e32 v202, v202, v202
	v_max_f32_e32 v203, v203, v203
	v_med3_f32 v170, v170, s20, v13
	v_med3_f32 v171, v171, s20, v13
	v_med3_f32 v172, v172, s20, v13
	v_med3_f32 v173, v173, s20, v13
	v_med3_f32 v174, v174, s20, v13
	v_med3_f32 v175, v175, s20, v13
	v_med3_f32 v176, v176, s20, v13
	v_med3_f32 v177, v177, s20, v13
	v_med3_f32 v196, v196, s20, v13
	v_med3_f32 v197, v197, s20, v13
	v_med3_f32 v198, v198, s20, v13
	v_med3_f32 v199, v199, s20, v13
	v_med3_f32 v200, v200, s20, v13
	v_med3_f32 v201, v201, s20, v13
	v_med3_f32 v202, v202, s20, v13
	v_med3_f32 v203, v203, s20, v13
	v_mov_b32_e32 v208, 0
	v_mov_b32_e32 v209, 0
	v_mov_b32_e32 v210, 0
	v_mov_b32_e32 v211, 0
	v_cvt_pk_fp8_f32 v208, v170, v171
	v_cvt_pk_fp8_f32 v209, v174, v175
	v_cvt_pk_fp8_f32 v210, v196, v197
	v_cvt_pk_fp8_f32 v211, v200, v201
	v_cvt_pk_fp8_f32 v208, v172, v173 op_sel:[0,0,1]
	v_cvt_pk_fp8_f32 v209, v176, v177 op_sel:[0,0,1]
	v_cvt_pk_fp8_f32 v210, v198, v199 op_sel:[0,0,1]
	v_cvt_pk_fp8_f32 v211, v202, v203 op_sel:[0,0,1]
	s_nop 0
	global_store_dwordx4 v28, v[208:211], s[14:15]
	ds_read_b32 v170, v8
	ds_read_b32 v171, v8 offset:512
	ds_read_b32 v172, v8 offset:1024
	ds_read_b32 v173, v8 offset:1536
	ds_read_b32 v174, v8 offset:2048
	ds_read_b32 v175, v8 offset:2560
	ds_read_b32 v176, v8 offset:3072
	ds_read_b32 v177, v8 offset:3584
	ds_read_b32 v196, v8 offset:4096
	ds_read_b32 v197, v8 offset:4608
	ds_read_b32 v198, v8 offset:5120
	ds_read_b32 v199, v8 offset:5632
	ds_read_b32 v200, v8 offset:6144
	ds_read_b32 v201, v8 offset:6656
	ds_read_b32 v202, v8 offset:7168
	ds_read_b32 v203, v8 offset:7680
	s_waitcnt lgkmcnt(0)
	v_max_f32_e32 v170, v170, v170
	v_max_f32_e32 v171, v171, v171
	v_max_f32_e32 v172, v172, v172
	v_max_f32_e32 v173, v173, v173
	v_max_f32_e32 v174, v174, v174
	v_max_f32_e32 v175, v175, v175
	v_max_f32_e32 v176, v176, v176
	v_max_f32_e32 v177, v177, v177
	v_max_f32_e32 v196, v196, v196
	v_max_f32_e32 v197, v197, v197
	v_max_f32_e32 v198, v198, v198
	v_max_f32_e32 v199, v199, v199
	v_max_f32_e32 v200, v200, v200
	v_max_f32_e32 v201, v201, v201
	v_max_f32_e32 v202, v202, v202
	v_max_f32_e32 v203, v203, v203
	v_med3_f32 v170, v170, s20, v13
	v_med3_f32 v171, v171, s20, v13
	v_med3_f32 v172, v172, s20, v13
	v_med3_f32 v173, v173, s20, v13
	v_med3_f32 v174, v174, s20, v13
	v_med3_f32 v175, v175, s20, v13
	v_med3_f32 v176, v176, s20, v13
	v_med3_f32 v177, v177, s20, v13
	v_med3_f32 v196, v196, s20, v13
	v_med3_f32 v197, v197, s20, v13
	v_med3_f32 v198, v198, s20, v13
	v_med3_f32 v199, v199, s20, v13
	v_med3_f32 v200, v200, s20, v13
	v_med3_f32 v201, v201, s20, v13
	v_med3_f32 v202, v202, s20, v13
	v_med3_f32 v203, v203, s20, v13
	v_mov_b32_e32 v208, 0
	v_mov_b32_e32 v209, 0
	v_mov_b32_e32 v210, 0
	v_mov_b32_e32 v211, 0
	v_cvt_pk_fp8_f32 v208, v170, v171
	v_cvt_pk_fp8_f32 v209, v174, v175
	v_cvt_pk_fp8_f32 v210, v196, v197
	v_cvt_pk_fp8_f32 v211, v200, v201
	v_cvt_pk_fp8_f32 v208, v172, v173 op_sel:[0,0,1]
	v_cvt_pk_fp8_f32 v209, v176, v177 op_sel:[0,0,1]
	v_cvt_pk_fp8_f32 v210, v198, v199 op_sel:[0,0,1]
	v_cvt_pk_fp8_f32 v211, v202, v203 op_sel:[0,0,1]
	s_nop 0
	global_store_dwordx4 v29, v[208:211], s[14:15]
	s_waitcnt vmcnt(32)
	v_mul_f32_e32 v132, v20, v132
	v_mul_f32_e32 v133, v20, v133
	v_mul_f32_e32 v134, v20, v134
	v_mul_f32_e32 v135, v20, v135
	ds_write_b128 v5, v[132:135]
	v_mul_f32_e32 v136, v21, v136
	v_mul_f32_e32 v137, v21, v137
	v_mul_f32_e32 v138, v21, v138
	v_mul_f32_e32 v139, v21, v139
	ds_write_b128 v5, v[136:139] offset:1024
	v_mul_f32_e32 v140, v22, v140
	v_mul_f32_e32 v141, v22, v141
	v_mul_f32_e32 v142, v22, v142
	v_mul_f32_e32 v143, v22, v143
	ds_write_b128 v5, v[140:143] offset:2048
	v_mul_f32_e32 v144, v23, v144
	v_mul_f32_e32 v145, v23, v145
	v_mul_f32_e32 v146, v23, v146
	v_mul_f32_e32 v147, v23, v147
	ds_write_b128 v5, v[144:147] offset:3072
	v_mul_f32_e32 v148, v24, v148
	v_mul_f32_e32 v149, v24, v149
	v_mul_f32_e32 v150, v24, v150
	v_mul_f32_e32 v151, v24, v151
	ds_write_b128 v5, v[148:151] offset:4096
	v_mul_f32_e32 v152, v25, v152
	v_mul_f32_e32 v153, v25, v153
	v_mul_f32_e32 v154, v25, v154
	v_mul_f32_e32 v155, v25, v155
	ds_write_b128 v5, v[152:155] offset:5120
	v_mul_f32_e32 v156, v26, v156
	v_mul_f32_e32 v157, v26, v157
	v_mul_f32_e32 v158, v26, v158
	v_mul_f32_e32 v159, v26, v159
	ds_write_b128 v5, v[156:159] offset:6144
	v_mul_f32_e32 v160, v27, v160
	v_mul_f32_e32 v161, v27, v161
	v_mul_f32_e32 v162, v27, v162
	v_mul_f32_e32 v163, v27, v163
	ds_write_b128 v5, v[160:163] offset:7168
	s_waitcnt lgkmcnt(0)
	s_barrier
; #define GAS __attribute__((address_space(1)))
; #define LAS __attribute__((address_space(3)))
; #define LDS_WAIT() asm volatile("s_waitcnt lgkmcnt(0)" ::: "memory")
;     const int pr = item >> 1, kb = 2 * (pr / nblk) + (item & 1), nb = pr % nblk, k0 = 64 * kb, n0 = 32 * nb;
;     const int nr = n0 + (lane & 31); const int sc = MAP == 1 ? src_col_in(nr) : nr;
;     float v[32];
; #pragma unroll
;     for (int i = 0; i < 32; ++i) v[i] = sc >= 0 ? W[(size_t)(k0 + 2 * i + (lane >> 5)) * Nsrc + sc] : 0.f;
; #pragma unroll
;     for (int i = 0; i < 32; ++i) { const int k = k0 + 2 * i + (lane >> 5); float x = v[i] * wscale; if (KS) x *= (k < ksplit ? ksA[k] : ksB[k - ksplit]); scr[(2 * i + (lane >> 5)) * 33 + (lane & 31)] = x; }
;     LDS_WAIT(); asm volatile("" ::: "memory");
;     const int c = lane & 7;
; #pragma unroll
;     for (int j = 0; j < 4; ++j) { const int n = (lane >> 3) + 8 * j; const LAS float* s = scr + (8 * c) * 33 + n;
;         const unsigned long long o = (unsigned long long)pg8::pk4_fp8(s[0 * 33], s[1 * 33], s[2 * 33], s[3 * 33]) | ((unsigned long long)pg8::pk4_fp8(s[4 * 33], s[5 * 33], s[6 * 33], s[7 * 33]) << 32);
;         *(GAS unsigned long long*)(WT + (size_t)(n0 + n) * K + k0 + 8 * c) = o; }
;     LDS_WAIT(); asm volatile("" ::: "memory");
; }
; __global__ void __launch_bounds__(NWAVES * 64, 2) hybrid_fwd(Args args) {
;     ...
;             if (r < I_UP) { p0_transpose_item_f8<true>(args.in[15] + (size_t)l * DM * FF, DM, FF, FF / 32, (unsigned char*)(ws + WS_WUP + l * SZ_WUP), WUP8_SCALE, args.in[14] + l * DM, args.in[14] + l * DM, DM, scr, r, lane); continue; } r -= I_UP;
	s_add_i32 s19, s39, 99
	s_min_u32 s19, s19, 127
	s_lshl_b32 s19, s19, 9
	s_add_u32 s12, s46, s19
	s_addc_u32 s13, s47, 0
	global_load_dwordx4 v[132:135], v30, s[12:13]
	s_add_u32 s12, s12, 0x20000
	s_addc_u32 s13, s13, 0
	global_load_dwordx4 v[136:139], v30, s[12:13]
	s_add_u32 s12, s12, 0x20000
	s_addc_u32 s13, s13, 0
	global_load_dwordx4 v[140:143], v30, s[12:13]
	s_add_u32 s12, s12, 0x20000
	s_addc_u32 s13, s13, 0
	global_load_dwordx4 v[144:147], v30, s[12:13]
	s_add_u32 s12, s12, 0x20000
	s_addc_u32 s13, s13, 0
	global_load_dwordx4 v[148:151], v30, s[12:13]
	s_add_u32 s12, s12, 0x20000
	s_addc_u32 s13, s13, 0
	global_load_dwordx4 v[152:155], v30, s[12:13]
	s_add_u32 s12, s12, 0x20000
	s_addc_u32 s13, s13, 0
	global_load_dwordx4 v[156:159], v30, s[12:13]
	s_add_u32 s12, s12, 0x20000
	s_addc_u32 s13, s13, 0
	global_load_dwordx4 v[160:163], v30, s[12:13]
	s_add_i32 s19, s39, 24
	s_min_u32 s19, s19, 31
	s_lshl_b32 s19, s19, 19
	s_add_u32 s14, s50, s19
	s_addc_u32 s15, s51, 0
	ds_read_b32 v170, v7
	ds_read_b32 v171, v7 offset:512
	ds_read_b32 v172, v7 offset:1024
	ds_read_b32 v173, v7 offset:1536
	ds_read_b32 v174, v7 offset:2048
	ds_read_b32 v175, v7 offset:2560
	ds_read_b32 v176, v7 offset:3072
	ds_read_b32 v177, v7 offset:3584
	ds_read_b32 v196, v7 offset:4096
	ds_read_b32 v197, v7 offset:4608
	ds_read_b32 v198, v7 offset:5120
	ds_read_b32 v199, v7 offset:5632
	ds_read_b32 v200, v7 offset:6144
	ds_read_b32 v201, v7 offset:6656
	ds_read_b32 v202, v7 offset:7168
	ds_read_b32 v203, v7 offset:7680
	s_waitcnt lgkmcnt(0)
	v_max_f32_e32 v170, v170, v170
	v_max_f32_e32 v171, v171, v171
	v_max_f32_e32 v172, v172, v172
	v_max_f32_e32 v173, v173, v173
	v_max_f32_e32 v174, v174, v174
	v_max_f32_e32 v175, v175, v175
	v_max_f32_e32 v176, v176, v176
	v_max_f32_e32 v177, v177, v177
	v_max_f32_e32 v196, v196, v196
	v_max_f32_e32 v197, v197, v197
	v_max_f32_e32 v198, v198, v198
	v_max_f32_e32 v199, v199, v199
	v_max_f32_e32 v200, v200, v200
	v_max_f32_e32 v201, v201, v201
	v_max_f32_e32 v202, v202, v202
	v_max_f32_e32 v203, v203, v203
	v_med3_f32 v170, v170, s20, v13
	v_med3_f32 v171, v171, s20, v13
	v_med3_f32 v172, v172, s20, v13
	v_med3_f32 v173, v173, s20, v13
	v_med3_f32 v174, v174, s20, v13
	v_med3_f32 v175, v175, s20, v13
	v_med3_f32 v176, v176, s20, v13
	v_med3_f32 v177, v177, s20, v13
	v_med3_f32 v196, v196, s20, v13
	v_med3_f32 v197, v197, s20, v13
	v_med3_f32 v198, v198, s20, v13
	v_med3_f32 v199, v199, s20, v13
	v_med3_f32 v200, v200, s20, v13
	v_med3_f32 v201, v201, s20, v13
	v_med3_f32 v202, v202, s20, v13
	v_med3_f32 v203, v203, s20, v13
	v_mov_b32_e32 v208, 0
	v_mov_b32_e32 v209, 0
	v_mov_b32_e32 v210, 0
	v_mov_b32_e32 v211, 0
	v_cvt_pk_fp8_f32 v208, v170, v171
	v_cvt_pk_fp8_f32 v209, v174, v175
	v_cvt_pk_fp8_f32 v210, v196, v197
	v_cvt_pk_fp8_f32 v211, v200, v201
	v_cvt_pk_fp8_f32 v208, v172, v173 op_sel:[0,0,1]
	v_cvt_pk_fp8_f32 v209, v176, v177 op_sel:[0,0,1]
	v_cvt_pk_fp8_f32 v210, v198, v199 op_sel:[0,0,1]
	v_cvt_pk_fp8_f32 v211, v202, v203 op_sel:[0,0,1]
	s_nop 0
	global_store_dwordx4 v28, v[208:211], s[14:15]
	ds_read_b32 v170, v9
	ds_read_b32 v171, v9 offset:512
	ds_read_b32 v172, v9 offset:1024
	ds_read_b32 v173, v9 offset:1536
	ds_read_b32 v174, v9 offset:2048
	ds_read_b32 v175, v9 offset:2560
	ds_read_b32 v176, v9 offset:3072
	ds_read_b32 v177, v9 offset:3584
	ds_read_b32 v196, v9 offset:4096
	ds_read_b32 v197, v9 offset:4608
	ds_read_b32 v198, v9 offset:5120
	ds_read_b32 v199, v9 offset:5632
	ds_read_b32 v200, v9 offset:6144
	ds_read_b32 v201, v9 offset:6656
	ds_read_b32 v202, v9 offset:7168
	ds_read_b32 v203, v9 offset:7680
	s_waitcnt lgkmcnt(0)
	v_max_f32_e32 v170, v170, v170
	v_max_f32_e32 v171, v171, v171
	v_max_f32_e32 v172, v172, v172
	v_max_f32_e32 v173, v173, v173
	v_max_f32_e32 v174, v174, v174
	v_max_f32_e32 v175, v175, v175
	v_max_f32_e32 v176, v176, v176
	v_max_f32_e32 v177, v177, v177
	v_max_f32_e32 v196, v196, v196
	v_max_f32_e32 v197, v197, v197
	v_max_f32_e32 v198, v198, v198
	v_max_f32_e32 v199, v199, v199
	v_max_f32_e32 v200, v200, v200
	v_max_f32_e32 v201, v201, v201
	v_max_f32_e32 v202, v202, v202
	v_max_f32_e32 v203, v203, v203
	v_med3_f32 v170, v170, s20, v13
	v_med3_f32 v171, v171, s20, v13
	v_med3_f32 v172, v172, s20, v13
	v_med3_f32 v173, v173, s20, v13
	v_med3_f32 v174, v174, s20, v13
	v_med3_f32 v175, v175, s20, v13
	v_med3_f32 v176, v176, s20, v13
	v_med3_f32 v177, v177, s20, v13
	v_med3_f32 v196, v196, s20, v13
	v_med3_f32 v197, v197, s20, v13
	v_med3_f32 v198, v198, s20, v13
	v_med3_f32 v199, v199, s20, v13
	v_med3_f32 v200, v200, s20, v13
	v_med3_f32 v201, v201, s20, v13
	v_med3_f32 v202, v202, s20, v13
	v_med3_f32 v203, v203, s20, v13
	v_mov_b32_e32 v208, 0
	v_mov_b32_e32 v209, 0
	v_mov_b32_e32 v210, 0
	v_mov_b32_e32 v211, 0
	v_cvt_pk_fp8_f32 v208, v170, v171
	v_cvt_pk_fp8_f32 v209, v174, v175
	v_cvt_pk_fp8_f32 v210, v196, v197
	v_cvt_pk_fp8_f32 v211, v200, v201
	v_cvt_pk_fp8_f32 v208, v172, v173 op_sel:[0,0,1]
	v_cvt_pk_fp8_f32 v209, v176, v177 op_sel:[0,0,1]
	v_cvt_pk_fp8_f32 v210, v198, v199 op_sel:[0,0,1]
	v_cvt_pk_fp8_f32 v211, v202, v203 op_sel:[0,0,1]
	s_nop 0
	global_store_dwordx4 v29, v[208:211], s[14:15]
	s_waitcnt vmcnt(32)
	v_mul_f32_e32 v36, v20, v36
	v_mul_f32_e32 v37, v20, v37
	v_mul_f32_e32 v38, v20, v38
	v_mul_f32_e32 v39, v20, v39
	ds_write_b128 v4, v[36:39]
	v_mul_f32_e32 v40, v21, v40
	v_mul_f32_e32 v41, v21, v41
	v_mul_f32_e32 v42, v21, v42
	v_mul_f32_e32 v43, v21, v43
	ds_write_b128 v4, v[40:43] offset:1024
	v_mul_f32_e32 v44, v22, v44
	v_mul_f32_e32 v45, v22, v45
	v_mul_f32_e32 v46, v22, v46
	v_mul_f32_e32 v47, v22, v47
	ds_write_b128 v4, v[44:47] offset:2048
	v_mul_f32_e32 v48, v23, v48
	v_mul_f32_e32 v49, v23, v49
	v_mul_f32_e32 v50, v23, v50
	v_mul_f32_e32 v51, v23, v51
	ds_write_b128 v4, v[48:51] offset:3072
	v_mul_f32_e32 v52, v24, v52
	v_mul_f32_e32 v53, v24, v53
	v_mul_f32_e32 v54, v24, v54
	v_mul_f32_e32 v55, v24, v55
	ds_write_b128 v4, v[52:55] offset:4096
	v_mul_f32_e32 v56, v25, v56
	v_mul_f32_e32 v57, v25, v57
	v_mul_f32_e32 v58, v25, v58
	v_mul_f32_e32 v59, v25, v59
	ds_write_b128 v4, v[56:59] offset:5120
	v_mul_f32_e32 v60, v26, v60
	v_mul_f32_e32 v61, v26, v61
	v_mul_f32_e32 v62, v26, v62
	v_mul_f32_e32 v63, v26, v63
	ds_write_b128 v4, v[60:63] offset:6144
	v_mul_f32_e32 v64, v27, v64
	v_mul_f32_e32 v65, v27, v65
	v_mul_f32_e32 v66, v27, v66
	v_mul_f32_e32 v67, v27, v67
	ds_write_b128 v4, v[64:67] offset:7168
	s_waitcnt lgkmcnt(0)
	s_barrier
; #define GAS __attribute__((address_space(1)))
; #define LAS __attribute__((address_space(3)))
; #define LDS_WAIT() asm volatile("s_waitcnt lgkmcnt(0)" ::: "memory")
;     const int pr = item >> 1, kb = 2 * (pr / nblk) + (item & 1), nb = pr % nblk, k0 = 64 * kb, n0 = 32 * nb;
;     const int nr = n0 + (lane & 31); const int sc = MAP == 1 ? src_col_in(nr) : nr;
;     float v[32];
; #pragma unroll
;     for (int i = 0; i < 32; ++i) v[i] = sc >= 0 ? W[(size_t)(k0 + 2 * i + (lane >> 5)) * Nsrc + sc] : 0.f;
; #pragma unroll
;     for (int i = 0; i < 32; ++i) { const int k = k0 + 2 * i + (lane >> 5); float x = v[i] * wscale; if (KS) x *= (k < ksplit ? ksA[k] : ksB[k - ksplit]); scr[(2 * i + (lane >> 5)) * 33 + (lane & 31)] = x; }
;     LDS_WAIT(); asm volatile("" ::: "memory");
;     const int c = lane & 7;
; #pragma unroll
;     for (int j = 0; j < 4; ++j) { const int n = (lane >> 3) + 8 * j; const LAS float* s = scr + (8 * c) * 33 + n;
;         const unsigned long long o = (unsigned long long)pg8::pk4_fp8(s[0 * 33], s[1 * 33], s[2 * 33], s[3 * 33]) | ((unsigned long long)pg8::pk4_fp8(s[4 * 33], s[5 * 33], s[6 * 33], s[7 * 33]) << 32);
;         *(GAS unsigned long long*)(WT + (size_t)(n0 + n) * K + k0 + 8 * c) = o; }
;     LDS_WAIT(); asm volatile("" ::: "memory");
; }
; __global__ void __launch_bounds__(NWAVES * 64, 2) hybrid_fwd(Args args) {
;     ...
;             if (r < I_UP) { p0_transpose_item_f8<true>(args.in[15] + (size_t)l * DM * FF, DM, FF, FF / 32, (unsigned char*)(ws + WS_WUP + l * SZ_WUP), WUP8_SCALE, args.in[14] + l * DM, args.in[14] + l * DM, DM, scr, r, lane); continue; } r -= I_UP;
	s_add_i32 s19, s39, 102
	s_min_u32 s19, s19, 127
	s_lshl_b32 s19, s19, 9
	s_add_u32 s12, s46, s19
	s_addc_u32 s13, s47, 0
	global_load_dwordx4 v[36:39], v30, s[12:13]
	s_add_u32 s12, s12, 0x20000
	s_addc_u32 s13, s13, 0
	global_load_dwordx4 v[40:43], v30, s[12:13]
	s_add_u32 s12, s12, 0x20000
	s_addc_u32 s13, s13, 0
	global_load_dwordx4 v[44:47], v30, s[12:13]
	s_add_u32 s12, s12, 0x20000
	s_addc_u32 s13, s13, 0
	global_load_dwordx4 v[48:51], v30, s[12:13]
	s_add_u32 s12, s12, 0x20000
	s_addc_u32 s13, s13, 0
	global_load_dwordx4 v[52:55], v30, s[12:13]
	s_add_u32 s12, s12, 0x20000
	s_addc_u32 s13, s13, 0
	global_load_dwordx4 v[56:59], v30, s[12:13]
	s_add_u32 s12, s12, 0x20000
	s_addc_u32 s13, s13, 0
	global_load_dwordx4 v[60:63], v30, s[12:13]
	s_add_u32 s12, s12, 0x20000
	s_addc_u32 s13, s13, 0
	global_load_dwordx4 v[64:67], v30, s[12:13]
	s_add_i32 s19, s39, 27
	s_min_u32 s19, s19, 31
	s_lshl_b32 s19, s19, 19
	s_add_u32 s14, s50, s19
	s_addc_u32 s15, s51, 0
	ds_read_b32 v170, v6
	ds_read_b32 v171, v6 offset:512
	ds_read_b32 v172, v6 offset:1024
	ds_read_b32 v173, v6 offset:1536
	ds_read_b32 v174, v6 offset:2048
	ds_read_b32 v175, v6 offset:2560
	ds_read_b32 v176, v6 offset:3072
	ds_read_b32 v177, v6 offset:3584
	ds_read_b32 v196, v6 offset:4096
	ds_read_b32 v197, v6 offset:4608
	ds_read_b32 v198, v6 offset:5120
	ds_read_b32 v199, v6 offset:5632
	ds_read_b32 v200, v6 offset:6144
	ds_read_b32 v201, v6 offset:6656
	ds_read_b32 v202, v6 offset:7168
	ds_read_b32 v203, v6 offset:7680
	s_waitcnt lgkmcnt(0)
	v_max_f32_e32 v170, v170, v170
	v_max_f32_e32 v171, v171, v171
	v_max_f32_e32 v172, v172, v172
	v_max_f32_e32 v173, v173, v173
	v_max_f32_e32 v174, v174, v174
	v_max_f32_e32 v175, v175, v175
	v_max_f32_e32 v176, v176, v176
	v_max_f32_e32 v177, v177, v177
	v_max_f32_e32 v196, v196, v196
	v_max_f32_e32 v197, v197, v197
	v_max_f32_e32 v198, v198, v198
	v_max_f32_e32 v199, v199, v199
	v_max_f32_e32 v200, v200, v200
	v_max_f32_e32 v201, v201, v201
	v_max_f32_e32 v202, v202, v202
	v_max_f32_e32 v203, v203, v203
	v_med3_f32 v170, v170, s20, v13
	v_med3_f32 v171, v171, s20, v13
	v_med3_f32 v172, v172, s20, v13
	v_med3_f32 v173, v173, s20, v13
	v_med3_f32 v174, v174, s20, v13
	v_med3_f32 v175, v175, s20, v13
	v_med3_f32 v176, v176, s20, v13
	v_med3_f32 v177, v177, s20, v13
	v_med3_f32 v196, v196, s20, v13
	v_med3_f32 v197, v197, s20, v13
	v_med3_f32 v198, v198, s20, v13
	v_med3_f32 v199, v199, s20, v13
	v_med3_f32 v200, v200, s20, v13
	v_med3_f32 v201, v201, s20, v13
	v_med3_f32 v202, v202, s20, v13
	v_med3_f32 v203, v203, s20, v13
	v_mov_b32_e32 v208, 0
	v_mov_b32_e32 v209, 0
	v_mov_b32_e32 v210, 0
	v_mov_b32_e32 v211, 0
	v_cvt_pk_fp8_f32 v208, v170, v171
	v_cvt_pk_fp8_f32 v209, v174, v175
	v_cvt_pk_fp8_f32 v210, v196, v197
	v_cvt_pk_fp8_f32 v211, v200, v201
	v_cvt_pk_fp8_f32 v208, v172, v173 op_sel:[0,0,1]
	v_cvt_pk_fp8_f32 v209, v176, v177 op_sel:[0,0,1]
	v_cvt_pk_fp8_f32 v210, v198, v199 op_sel:[0,0,1]
	v_cvt_pk_fp8_f32 v211, v202, v203 op_sel:[0,0,1]
	s_nop 0
	global_store_dwordx4 v28, v[208:211], s[14:15]
	ds_read_b32 v170, v8
	ds_read_b32 v171, v8 offset:512
	ds_read_b32 v172, v8 offset:1024
	ds_read_b32 v173, v8 offset:1536
	ds_read_b32 v174, v8 offset:2048
	ds_read_b32 v175, v8 offset:2560
	ds_read_b32 v176, v8 offset:3072
	ds_read_b32 v177, v8 offset:3584
	ds_read_b32 v196, v8 offset:4096
	ds_read_b32 v197, v8 offset:4608
	ds_read_b32 v198, v8 offset:5120
	ds_read_b32 v199, v8 offset:5632
	ds_read_b32 v200, v8 offset:6144
	ds_read_b32 v201, v8 offset:6656
	ds_read_b32 v202, v8 offset:7168
	ds_read_b32 v203, v8 offset:7680
	s_waitcnt lgkmcnt(0)
	v_max_f32_e32 v170, v170, v170
	v_max_f32_e32 v171, v171, v171
	v_max_f32_e32 v172, v172, v172
	v_max_f32_e32 v173, v173, v173
	v_max_f32_e32 v174, v174, v174
	v_max_f32_e32 v175, v175, v175
	v_max_f32_e32 v176, v176, v176
	v_max_f32_e32 v177, v177, v177
	v_max_f32_e32 v196, v196, v196
	v_max_f32_e32 v197, v197, v197
	v_max_f32_e32 v198, v198, v198
	v_max_f32_e32 v199, v199, v199
	v_max_f32_e32 v200, v200, v200
	v_max_f32_e32 v201, v201, v201
	v_max_f32_e32 v202, v202, v202
	v_max_f32_e32 v203, v203, v203
	v_med3_f32 v170, v170, s20, v13
	v_med3_f32 v171, v171, s20, v13
	v_med3_f32 v172, v172, s20, v13
	v_med3_f32 v173, v173, s20, v13
	v_med3_f32 v174, v174, s20, v13
	v_med3_f32 v175, v175, s20, v13
	v_med3_f32 v176, v176, s20, v13
	v_med3_f32 v177, v177, s20, v13
	v_med3_f32 v196, v196, s20, v13
	v_med3_f32 v197, v197, s20, v13
	v_med3_f32 v198, v198, s20, v13
	v_med3_f32 v199, v199, s20, v13
	v_med3_f32 v200, v200, s20, v13
	v_med3_f32 v201, v201, s20, v13
	v_med3_f32 v202, v202, s20, v13
	v_med3_f32 v203, v203, s20, v13
	v_mov_b32_e32 v208, 0
	v_mov_b32_e32 v209, 0
	v_mov_b32_e32 v210, 0
	v_mov_b32_e32 v211, 0
	v_cvt_pk_fp8_f32 v208, v170, v171
	v_cvt_pk_fp8_f32 v209, v174, v175
	v_cvt_pk_fp8_f32 v210, v196, v197
	v_cvt_pk_fp8_f32 v211, v200, v201
	v_cvt_pk_fp8_f32 v208, v172, v173 op_sel:[0,0,1]
	v_cvt_pk_fp8_f32 v209, v176, v177 op_sel:[0,0,1]
	v_cvt_pk_fp8_f32 v210, v198, v199 op_sel:[0,0,1]
	v_cvt_pk_fp8_f32 v211, v202, v203 op_sel:[0,0,1]
	s_nop 0
	global_store_dwordx4 v29, v[208:211], s[14:15]
	s_waitcnt vmcnt(32)
	v_mul_f32_e32 v68, v20, v68
	v_mul_f32_e32 v69, v20, v69
	v_mul_f32_e32 v70, v20, v70
	v_mul_f32_e32 v71, v20, v71
	ds_write_b128 v5, v[68:71]
	v_mul_f32_e32 v72, v21, v72
	v_mul_f32_e32 v73, v21, v73
	v_mul_f32_e32 v74, v21, v74
	v_mul_f32_e32 v75, v21, v75
	ds_write_b128 v5, v[72:75] offset:1024
	v_mul_f32_e32 v76, v22, v76
	v_mul_f32_e32 v77, v22, v77
	v_mul_f32_e32 v78, v22, v78
	v_mul_f32_e32 v79, v22, v79
	ds_write_b128 v5, v[76:79] offset:2048
	v_mul_f32_e32 v80, v23, v80
	v_mul_f32_e32 v81, v23, v81
	v_mul_f32_e32 v82, v23, v82
	v_mul_f32_e32 v83, v23, v83
	ds_write_b128 v5, v[80:83] offset:3072
	v_mul_f32_e32 v84, v24, v84
	v_mul_f32_e32 v85, v24, v85
	v_mul_f32_e32 v86, v24, v86
	v_mul_f32_e32 v87, v24, v87
	ds_write_b128 v5, v[84:87] offset:4096
	v_mul_f32_e32 v88, v25, v88
	v_mul_f32_e32 v89, v25, v89
	v_mul_f32_e32 v90, v25, v90
	v_mul_f32_e32 v91, v25, v91
	ds_write_b128 v5, v[88:91] offset:5120
	v_mul_f32_e32 v92, v26, v92
	v_mul_f32_e32 v93, v26, v93
	v_mul_f32_e32 v94, v26, v94
	v_mul_f32_e32 v95, v26, v95
	ds_write_b128 v5, v[92:95] offset:6144
	v_mul_f32_e32 v96, v27, v96
	v_mul_f32_e32 v97, v27, v97
	v_mul_f32_e32 v98, v27, v98
	v_mul_f32_e32 v99, v27, v99
	ds_write_b128 v5, v[96:99] offset:7168
	s_waitcnt lgkmcnt(0)
	s_barrier
; #define GAS __attribute__((address_space(1)))
; #define LAS __attribute__((address_space(3)))
; #define LDS_WAIT() asm volatile("s_waitcnt lgkmcnt(0)" ::: "memory")
;     const int pr = item >> 1, kb = 2 * (pr / nblk) + (item & 1), nb = pr % nblk, k0 = 64 * kb, n0 = 32 * nb;
;     const int nr = n0 + (lane & 31); const int sc = MAP == 1 ? src_col_in(nr) : nr;
;     float v[32];
; #pragma unroll
;     for (int i = 0; i < 32; ++i) v[i] = sc >= 0 ? W[(size_t)(k0 + 2 * i + (lane >> 5)) * Nsrc + sc] : 0.f;
; #pragma unroll
;     for (int i = 0; i < 32; ++i) { const int k = k0 + 2 * i + (lane >> 5); float x = v[i] * wscale; if (KS) x *= (k < ksplit ? ksA[k] : ksB[k - ksplit]); scr[(2 * i + (lane >> 5)) * 33 + (lane & 31)] = x; }
;     LDS_WAIT(); asm volatile("" ::: "memory");
;     const int c = lane & 7;
; #pragma unroll
;     for (int j = 0; j < 4; ++j) { const int n = (lane >> 3) + 8 * j; const LAS float* s = scr + (8 * c) * 33 + n;
;         const unsigned long long o = (unsigned long long)pg8::pk4_fp8(s[0 * 33], s[1 * 33], s[2 * 33], s[3 * 33]) | ((unsigned long long)pg8::pk4_fp8(s[4 * 33], s[5 * 33], s[6 * 33], s[7 * 33]) << 32);
;         *(GAS unsigned long long*)(WT + (size_t)(n0 + n) * K + k0 + 8 * c) = o; }
;     LDS_WAIT(); asm volatile("" ::: "memory");
; }
; __global__ void __launch_bounds__(NWAVES * 64, 2) hybrid_fwd(Args args) {
;     ...
;             if (r < I_UP) { p0_transpose_item_f8<true>(args.in[15] + (size_t)l * DM * FF, DM, FF, FF / 32, (unsigned char*)(ws + WS_WUP + l * SZ_WUP), WUP8_SCALE, args.in[14] + l * DM, args.in[14] + l * DM, DM, scr, r, lane); continue; } r -= I_UP;
	s_add_i32 s19, s39, 105
	s_min_u32 s19, s19, 127
	s_lshl_b32 s19, s19, 9
	s_add_u32 s12, s46, s19
	s_addc_u32 s13, s47, 0
	global_load_dwordx4 v[68:71], v30, s[12:13]
	s_add_u32 s12, s12, 0x20000
	s_addc_u32 s13, s13, 0
	global_load_dwordx4 v[72:75], v30, s[12:13]
	s_add_u32 s12, s12, 0x20000
	s_addc_u32 s13, s13, 0
	global_load_dwordx4 v[76:79], v30, s[12:13]
	s_add_u32 s12, s12, 0x20000
	s_addc_u32 s13, s13, 0
	global_load_dwordx4 v[80:83], v30, s[12:13]
	s_add_u32 s12, s12, 0x20000
	s_addc_u32 s13, s13, 0
	global_load_dwordx4 v[84:87], v30, s[12:13]
	s_add_u32 s12, s12, 0x20000
	s_addc_u32 s13, s13, 0
	global_load_dwordx4 v[88:91], v30, s[12:13]
	s_add_u32 s12, s12, 0x20000
	s_addc_u32 s13, s13, 0
	global_load_dwordx4 v[92:95], v30, s[12:13]
	s_add_u32 s12, s12, 0x20000
	s_addc_u32 s13, s13, 0
	global_load_dwordx4 v[96:99], v30, s[12:13]
	s_add_i32 s19, s39, 30
	s_min_u32 s19, s19, 31
	s_lshl_b32 s19, s19, 19
	s_add_u32 s14, s50, s19
	s_addc_u32 s15, s51, 0
	ds_read_b32 v170, v7
	ds_read_b32 v171, v7 offset:512
	ds_read_b32 v172, v7 offset:1024
	ds_read_b32 v173, v7 offset:1536
	ds_read_b32 v174, v7 offset:2048
	ds_read_b32 v175, v7 offset:2560
	ds_read_b32 v176, v7 offset:3072
	ds_read_b32 v177, v7 offset:3584
	ds_read_b32 v196, v7 offset:4096
	ds_read_b32 v197, v7 offset:4608
	ds_read_b32 v198, v7 offset:5120
	ds_read_b32 v199, v7 offset:5632
	ds_read_b32 v200, v7 offset:6144
	ds_read_b32 v201, v7 offset:6656
	ds_read_b32 v202, v7 offset:7168
	ds_read_b32 v203, v7 offset:7680
	s_waitcnt lgkmcnt(0)
	v_max_f32_e32 v170, v170, v170
	v_max_f32_e32 v171, v171, v171
	v_max_f32_e32 v172, v172, v172
	v_max_f32_e32 v173, v173, v173
	v_max_f32_e32 v174, v174, v174
	v_max_f32_e32 v175, v175, v175
	v_max_f32_e32 v176, v176, v176
	v_max_f32_e32 v177, v177, v177
	v_max_f32_e32 v196, v196, v196
	v_max_f32_e32 v197, v197, v197
	v_max_f32_e32 v198, v198, v198
	v_max_f32_e32 v199, v199, v199
	v_max_f32_e32 v200, v200, v200
	v_max_f32_e32 v201, v201, v201
	v_max_f32_e32 v202, v202, v202
	v_max_f32_e32 v203, v203, v203
	v_med3_f32 v170, v170, s20, v13
	v_med3_f32 v171, v171, s20, v13
	v_med3_f32 v172, v172, s20, v13
	v_med3_f32 v173, v173, s20, v13
	v_med3_f32 v174, v174, s20, v13
	v_med3_f32 v175, v175, s20, v13
	v_med3_f32 v176, v176, s20, v13
	v_med3_f32 v177, v177, s20, v13
	v_med3_f32 v196, v196, s20, v13
	v_med3_f32 v197, v197, s20, v13
	v_med3_f32 v198, v198, s20, v13
	v_med3_f32 v199, v199, s20, v13
	v_med3_f32 v200, v200, s20, v13
	v_med3_f32 v201, v201, s20, v13
	v_med3_f32 v202, v202, s20, v13
	v_med3_f32 v203, v203, s20, v13
	v_mov_b32_e32 v208, 0
	v_mov_b32_e32 v209, 0
	v_mov_b32_e32 v210, 0
	v_mov_b32_e32 v211, 0
	v_cvt_pk_fp8_f32 v208, v170, v171
	v_cvt_pk_fp8_f32 v209, v174, v175
	v_cvt_pk_fp8_f32 v210, v196, v197
	v_cvt_pk_fp8_f32 v211, v200, v201
	v_cvt_pk_fp8_f32 v208, v172, v173 op_sel:[0,0,1]
	v_cvt_pk_fp8_f32 v209, v176, v177 op_sel:[0,0,1]
	v_cvt_pk_fp8_f32 v210, v198, v199 op_sel:[0,0,1]
	v_cvt_pk_fp8_f32 v211, v202, v203 op_sel:[0,0,1]
	s_nop 0
	global_store_dwordx4 v28, v[208:211], s[14:15]
	ds_read_b32 v170, v9
	ds_read_b32 v171, v9 offset:512
	ds_read_b32 v172, v9 offset:1024
	ds_read_b32 v173, v9 offset:1536
	ds_read_b32 v174, v9 offset:2048
	ds_read_b32 v175, v9 offset:2560
	ds_read_b32 v176, v9 offset:3072
	ds_read_b32 v177, v9 offset:3584
	ds_read_b32 v196, v9 offset:4096
	ds_read_b32 v197, v9 offset:4608
	ds_read_b32 v198, v9 offset:5120
	ds_read_b32 v199, v9 offset:5632
	ds_read_b32 v200, v9 offset:6144
	ds_read_b32 v201, v9 offset:6656
	ds_read_b32 v202, v9 offset:7168
	ds_read_b32 v203, v9 offset:7680
	s_waitcnt lgkmcnt(0)
	v_max_f32_e32 v170, v170, v170
	v_max_f32_e32 v171, v171, v171
	v_max_f32_e32 v172, v172, v172
	v_max_f32_e32 v173, v173, v173
	v_max_f32_e32 v174, v174, v174
	v_max_f32_e32 v175, v175, v175
	v_max_f32_e32 v176, v176, v176
	v_max_f32_e32 v177, v177, v177
	v_max_f32_e32 v196, v196, v196
	v_max_f32_e32 v197, v197, v197
	v_max_f32_e32 v198, v198, v198
	v_max_f32_e32 v199, v199, v199
	v_max_f32_e32 v200, v200, v200
	v_max_f32_e32 v201, v201, v201
	v_max_f32_e32 v202, v202, v202
	v_max_f32_e32 v203, v203, v203
	v_med3_f32 v170, v170, s20, v13
	v_med3_f32 v171, v171, s20, v13
	v_med3_f32 v172, v172, s20, v13
	v_med3_f32 v173, v173, s20, v13
	v_med3_f32 v174, v174, s20, v13
	v_med3_f32 v175, v175, s20, v13
	v_med3_f32 v176, v176, s20, v13
	v_med3_f32 v177, v177, s20, v13
	v_med3_f32 v196, v196, s20, v13
	v_med3_f32 v197, v197, s20, v13
	v_med3_f32 v198, v198, s20, v13
	v_med3_f32 v199, v199, s20, v13
	v_med3_f32 v200, v200, s20, v13
	v_med3_f32 v201, v201, s20, v13
	v_med3_f32 v202, v202, s20, v13
	v_med3_f32 v203, v203, s20, v13
	v_mov_b32_e32 v208, 0
	v_mov_b32_e32 v209, 0
	v_mov_b32_e32 v210, 0
	v_mov_b32_e32 v211, 0
	v_cvt_pk_fp8_f32 v208, v170, v171
	v_cvt_pk_fp8_f32 v209, v174, v175
	v_cvt_pk_fp8_f32 v210, v196, v197
	v_cvt_pk_fp8_f32 v211, v200, v201
	v_cvt_pk_fp8_f32 v208, v172, v173 op_sel:[0,0,1]
	v_cvt_pk_fp8_f32 v209, v176, v177 op_sel:[0,0,1]
	v_cvt_pk_fp8_f32 v210, v198, v199 op_sel:[0,0,1]
	v_cvt_pk_fp8_f32 v211, v202, v203 op_sel:[0,0,1]
	s_nop 0
	global_store_dwordx4 v29, v[208:211], s[14:15]
	s_waitcnt vmcnt(32)
	v_mul_f32_e32 v100, v232, v100
	v_mul_f32_e32 v101, v232, v101
	v_mul_f32_e32 v102, v232, v102
	v_mul_f32_e32 v103, v232, v103
	ds_write_b128 v4, v[100:103]
	v_mul_f32_e32 v104, v233, v104
	v_mul_f32_e32 v105, v233, v105
	v_mul_f32_e32 v106, v233, v106
	v_mul_f32_e32 v107, v233, v107
	ds_write_b128 v4, v[104:107] offset:1024
	v_mul_f32_e32 v108, v234, v108
	v_mul_f32_e32 v109, v234, v109
	v_mul_f32_e32 v110, v234, v110
	v_mul_f32_e32 v111, v234, v111
	ds_write_b128 v4, v[108:111] offset:2048
	v_mul_f32_e32 v112, v235, v112
	v_mul_f32_e32 v113, v235, v113
	v_mul_f32_e32 v114, v235, v114
	v_mul_f32_e32 v115, v235, v115
	ds_write_b128 v4, v[112:115] offset:3072
	v_mul_f32_e32 v116, v236, v116
	v_mul_f32_e32 v117, v236, v117
	v_mul_f32_e32 v118, v236, v118
	v_mul_f32_e32 v119, v236, v119
	ds_write_b128 v4, v[116:119] offset:4096
	v_mul_f32_e32 v120, v237, v120
	v_mul_f32_e32 v121, v237, v121
	v_mul_f32_e32 v122, v237, v122
	v_mul_f32_e32 v123, v237, v123
	ds_write_b128 v4, v[120:123] offset:5120
	v_mul_f32_e32 v124, v238, v124
	v_mul_f32_e32 v125, v238, v125
	v_mul_f32_e32 v126, v238, v126
	v_mul_f32_e32 v127, v238, v127
	ds_write_b128 v4, v[124:127] offset:6144
	v_mul_f32_e32 v128, v239, v128
	v_mul_f32_e32 v129, v239, v129
	v_mul_f32_e32 v130, v239, v130
	v_mul_f32_e32 v131, v239, v131
	ds_write_b128 v4, v[128:131] offset:7168
	s_waitcnt lgkmcnt(0)
	s_barrier
; #define GAS __attribute__((address_space(1)))
; #define LAS __attribute__((address_space(3)))
; #define LDS_WAIT() asm volatile("s_waitcnt lgkmcnt(0)" ::: "memory")
;     const int pr = item >> 1, kb = 2 * (pr / nblk) + (item & 1), nb = pr % nblk, k0 = 64 * kb, n0 = 32 * nb;
;     const int nr = n0 + (lane & 31); const int sc = MAP == 1 ? src_col_in(nr) : nr;
;     float v[32];
; #pragma unroll
;     for (int i = 0; i < 32; ++i) v[i] = sc >= 0 ? W[(size_t)(k0 + 2 * i + (lane >> 5)) * Nsrc + sc] : 0.f;
; #pragma unroll
;     for (int i = 0; i < 32; ++i) { const int k = k0 + 2 * i + (lane >> 5); float x = v[i] * wscale; if (KS) x *= (k < ksplit ? ksA[k] : ksB[k - ksplit]); scr[(2 * i + (lane >> 5)) * 33 + (lane & 31)] = x; }
;     LDS_WAIT(); asm volatile("" ::: "memory");
;     const int c = lane & 7;
; #pragma unroll
;     for (int j = 0; j < 4; ++j) { const int n = (lane >> 3) + 8 * j; const LAS float* s = scr + (8 * c) * 33 + n;
;         const unsigned long long o = (unsigned long long)pg8::pk4_fp8(s[0 * 33], s[1 * 33], s[2 * 33], s[3 * 33]) | ((unsigned long long)pg8::pk4_fp8(s[4 * 33], s[5 * 33], s[6 * 33], s[7 * 33]) << 32);
;         *(GAS unsigned long long*)(WT + (size_t)(n0 + n) * K + k0 + 8 * c) = o; }
;     LDS_WAIT(); asm volatile("" ::: "memory");
; }
; __global__ void __launch_bounds__(NWAVES * 64, 2) hybrid_fwd(Args args) {
;     ...
;             if (r < I_UP) { p0_transpose_item_f8<true>(args.in[15] + (size_t)l * DM * FF, DM, FF, FF / 32, (unsigned char*)(ws + WS_WUP + l * SZ_WUP), WUP8_SCALE, args.in[14] + l * DM, args.in[14] + l * DM, DM, scr, r, lane); continue; } r -= I_UP;
	s_add_i32 s19, s39, 108
	s_min_u32 s19, s19, 127
	s_lshl_b32 s19, s19, 9
	s_add_u32 s12, s46, s19
	s_addc_u32 s13, s47, 0
	global_load_dwordx4 v[100:103], v30, s[12:13]
	s_add_u32 s12, s12, 0x20000
	s_addc_u32 s13, s13, 0
	global_load_dwordx4 v[104:107], v30, s[12:13]
	s_add_u32 s12, s12, 0x20000
	s_addc_u32 s13, s13, 0
	global_load_dwordx4 v[108:111], v30, s[12:13]
	s_add_u32 s12, s12, 0x20000
	s_addc_u32 s13, s13, 0
	global_load_dwordx4 v[112:115], v30, s[12:13]
	s_add_u32 s12, s12, 0x20000
	s_addc_u32 s13, s13, 0
	global_load_dwordx4 v[116:119], v30, s[12:13]
	s_add_u32 s12, s12, 0x20000
	s_addc_u32 s13, s13, 0
	global_load_dwordx4 v[120:123], v30, s[12:13]
	s_add_u32 s12, s12, 0x20000
	s_addc_u32 s13, s13, 0
	global_load_dwordx4 v[124:127], v30, s[12:13]
	s_add_u32 s12, s12, 0x20000
	s_addc_u32 s13, s13, 0
	global_load_dwordx4 v[128:131], v30, s[12:13]
	s_add_i32 s19, s39, 96
	s_min_u32 s19, s19, 127
	s_lshl_b32 s19, s19, 19
	s_add_u32 s14, s64, s19
	s_addc_u32 s15, s65, 0
	ds_read_b32 v170, v6
	ds_read_b32 v171, v6 offset:512
	ds_read_b32 v172, v6 offset:1024
	ds_read_b32 v173, v6 offset:1536
	ds_read_b32 v174, v6 offset:2048
	ds_read_b32 v175, v6 offset:2560
	ds_read_b32 v176, v6 offset:3072
	ds_read_b32 v177, v6 offset:3584
	ds_read_b32 v196, v6 offset:4096
	ds_read_b32 v197, v6 offset:4608
	ds_read_b32 v198, v6 offset:5120
	ds_read_b32 v199, v6 offset:5632
	ds_read_b32 v200, v6 offset:6144
	ds_read_b32 v201, v6 offset:6656
	ds_read_b32 v202, v6 offset:7168
	ds_read_b32 v203, v6 offset:7680
	s_waitcnt lgkmcnt(0)
	v_max_f32_e32 v170, v170, v170
	v_max_f32_e32 v171, v171, v171
	v_max_f32_e32 v172, v172, v172
	v_max_f32_e32 v173, v173, v173
	v_max_f32_e32 v174, v174, v174
	v_max_f32_e32 v175, v175, v175
	v_max_f32_e32 v176, v176, v176
	v_max_f32_e32 v177, v177, v177
	v_max_f32_e32 v196, v196, v196
	v_max_f32_e32 v197, v197, v197
	v_max_f32_e32 v198, v198, v198
	v_max_f32_e32 v199, v199, v199
	v_max_f32_e32 v200, v200, v200
	v_max_f32_e32 v201, v201, v201
	v_max_f32_e32 v202, v202, v202
	v_max_f32_e32 v203, v203, v203
	v_med3_f32 v170, v170, s20, v13
	v_med3_f32 v171, v171, s20, v13
	v_med3_f32 v172, v172, s20, v13
	v_med3_f32 v173, v173, s20, v13
	v_med3_f32 v174, v174, s20, v13
	v_med3_f32 v175, v175, s20, v13
	v_med3_f32 v176, v176, s20, v13
	v_med3_f32 v177, v177, s20, v13
	v_med3_f32 v196, v196, s20, v13
	v_med3_f32 v197, v197, s20, v13
	v_med3_f32 v198, v198, s20, v13
	v_med3_f32 v199, v199, s20, v13
	v_med3_f32 v200, v200, s20, v13
	v_med3_f32 v201, v201, s20, v13
	v_med3_f32 v202, v202, s20, v13
	v_med3_f32 v203, v203, s20, v13
	v_mov_b32_e32 v208, 0
	v_mov_b32_e32 v209, 0
	v_mov_b32_e32 v210, 0
	v_mov_b32_e32 v211, 0
	v_cvt_pk_fp8_f32 v208, v170, v171
	v_cvt_pk_fp8_f32 v209, v174, v175
	v_cvt_pk_fp8_f32 v210, v196, v197
	v_cvt_pk_fp8_f32 v211, v200, v201
	v_cvt_pk_fp8_f32 v208, v172, v173 op_sel:[0,0,1]
	v_cvt_pk_fp8_f32 v209, v176, v177 op_sel:[0,0,1]
	v_cvt_pk_fp8_f32 v210, v198, v199 op_sel:[0,0,1]
	v_cvt_pk_fp8_f32 v211, v202, v203 op_sel:[0,0,1]
	s_nop 0
	global_store_dwordx4 v28, v[208:211], s[14:15]
	ds_read_b32 v170, v8
	ds_read_b32 v171, v8 offset:512
	ds_read_b32 v172, v8 offset:1024
	ds_read_b32 v173, v8 offset:1536
	ds_read_b32 v174, v8 offset:2048
	ds_read_b32 v175, v8 offset:2560
	ds_read_b32 v176, v8 offset:3072
	ds_read_b32 v177, v8 offset:3584
	ds_read_b32 v196, v8 offset:4096
	ds_read_b32 v197, v8 offset:4608
	ds_read_b32 v198, v8 offset:5120
	ds_read_b32 v199, v8 offset:5632
	ds_read_b32 v200, v8 offset:6144
	ds_read_b32 v201, v8 offset:6656
	ds_read_b32 v202, v8 offset:7168
	ds_read_b32 v203, v8 offset:7680
	s_waitcnt lgkmcnt(0)
	v_max_f32_e32 v170, v170, v170
	v_max_f32_e32 v171, v171, v171
	v_max_f32_e32 v172, v172, v172
	v_max_f32_e32 v173, v173, v173
	v_max_f32_e32 v174, v174, v174
	v_max_f32_e32 v175, v175, v175
	v_max_f32_e32 v176, v176, v176
	v_max_f32_e32 v177, v177, v177
	v_max_f32_e32 v196, v196, v196
	v_max_f32_e32 v197, v197, v197
	v_max_f32_e32 v198, v198, v198
	v_max_f32_e32 v199, v199, v199
	v_max_f32_e32 v200, v200, v200
	v_max_f32_e32 v201, v201, v201
	v_max_f32_e32 v202, v202, v202
	v_max_f32_e32 v203, v203, v203
	v_med3_f32 v170, v170, s20, v13
	v_med3_f32 v171, v171, s20, v13
	v_med3_f32 v172, v172, s20, v13
	v_med3_f32 v173, v173, s20, v13
	v_med3_f32 v174, v174, s20, v13
	v_med3_f32 v175, v175, s20, v13
	v_med3_f32 v176, v176, s20, v13
	v_med3_f32 v177, v177, s20, v13
	v_med3_f32 v196, v196, s20, v13
	v_med3_f32 v197, v197, s20, v13
	v_med3_f32 v198, v198, s20, v13
	v_med3_f32 v199, v199, s20, v13
	v_med3_f32 v200, v200, s20, v13
	v_med3_f32 v201, v201, s20, v13
	v_med3_f32 v202, v202, s20, v13
	v_med3_f32 v203, v203, s20, v13
	v_mov_b32_e32 v208, 0
	v_mov_b32_e32 v209, 0
	v_mov_b32_e32 v210, 0
	v_mov_b32_e32 v211, 0
	v_cvt_pk_fp8_f32 v208, v170, v171
	v_cvt_pk_fp8_f32 v209, v174, v175
	v_cvt_pk_fp8_f32 v210, v196, v197
	v_cvt_pk_fp8_f32 v211, v200, v201
	v_cvt_pk_fp8_f32 v208, v172, v173 op_sel:[0,0,1]
	v_cvt_pk_fp8_f32 v209, v176, v177 op_sel:[0,0,1]
	v_cvt_pk_fp8_f32 v210, v198, v199 op_sel:[0,0,1]
	v_cvt_pk_fp8_f32 v211, v202, v203 op_sel:[0,0,1]
	s_nop 0
	global_store_dwordx4 v29, v[208:211], s[14:15]
	s_waitcnt vmcnt(32)
	v_mul_f32_e32 v132, v232, v132
	v_mul_f32_e32 v133, v232, v133
	v_mul_f32_e32 v134, v232, v134
	v_mul_f32_e32 v135, v232, v135
	ds_write_b128 v5, v[132:135]
	v_mul_f32_e32 v136, v233, v136
	v_mul_f32_e32 v137, v233, v137
	v_mul_f32_e32 v138, v233, v138
	v_mul_f32_e32 v139, v233, v139
	ds_write_b128 v5, v[136:139] offset:1024
	v_mul_f32_e32 v140, v234, v140
	v_mul_f32_e32 v141, v234, v141
	v_mul_f32_e32 v142, v234, v142
	v_mul_f32_e32 v143, v234, v143
	ds_write_b128 v5, v[140:143] offset:2048
	v_mul_f32_e32 v144, v235, v144
	v_mul_f32_e32 v145, v235, v145
	v_mul_f32_e32 v146, v235, v146
	v_mul_f32_e32 v147, v235, v147
	ds_write_b128 v5, v[144:147] offset:3072
	v_mul_f32_e32 v148, v236, v148
	v_mul_f32_e32 v149, v236, v149
	v_mul_f32_e32 v150, v236, v150
	v_mul_f32_e32 v151, v236, v151
	ds_write_b128 v5, v[148:151] offset:4096
	v_mul_f32_e32 v152, v237, v152
	v_mul_f32_e32 v153, v237, v153
	v_mul_f32_e32 v154, v237, v154
	v_mul_f32_e32 v155, v237, v155
	ds_write_b128 v5, v[152:155] offset:5120
	v_mul_f32_e32 v156, v238, v156
	v_mul_f32_e32 v157, v238, v157
	v_mul_f32_e32 v158, v238, v158
	v_mul_f32_e32 v159, v238, v159
	ds_write_b128 v5, v[156:159] offset:6144
	v_mul_f32_e32 v160, v239, v160
	v_mul_f32_e32 v161, v239, v161
	v_mul_f32_e32 v162, v239, v162
	v_mul_f32_e32 v163, v239, v163
	ds_write_b128 v5, v[160:163] offset:7168
	s_waitcnt lgkmcnt(0)
	s_barrier
; #define GAS __attribute__((address_space(1)))
; #define LAS __attribute__((address_space(3)))
; #define LDS_WAIT() asm volatile("s_waitcnt lgkmcnt(0)" ::: "memory")
;     const int pr = item >> 1, kb = 2 * (pr / nblk) + (item & 1), nb = pr % nblk, k0 = 64 * kb, n0 = 32 * nb;
;     const int nr = n0 + (lane & 31); const int sc = MAP == 1 ? src_col_in(nr) : nr;
;     float v[32];
; #pragma unroll
;     for (int i = 0; i < 32; ++i) v[i] = sc >= 0 ? W[(size_t)(k0 + 2 * i + (lane >> 5)) * Nsrc + sc] : 0.f;
; #pragma unroll
;     for (int i = 0; i < 32; ++i) { const int k = k0 + 2 * i + (lane >> 5); float x = v[i] * wscale; if (KS) x *= (k < ksplit ? ksA[k] : ksB[k - ksplit]); scr[(2 * i + (lane >> 5)) * 33 + (lane & 31)] = x; }
;     LDS_WAIT(); asm volatile("" ::: "memory");
;     const int c = lane & 7;
; #pragma unroll
;     for (int j = 0; j < 4; ++j) { const int n = (lane >> 3) + 8 * j; const LAS float* s = scr + (8 * c) * 33 + n;
;         const unsigned long long o = (unsigned long long)pg8::pk4_fp8(s[0 * 33], s[1 * 33], s[2 * 33], s[3 * 33]) | ((unsigned long long)pg8::pk4_fp8(s[4 * 33], s[5 * 33], s[6 * 33], s[7 * 33]) << 32);
;         *(GAS unsigned long long*)(WT + (size_t)(n0 + n) * K + k0 + 8 * c) = o; }
;     LDS_WAIT(); asm volatile("" ::: "memory");
; }
; __global__ void __launch_bounds__(NWAVES * 64, 2) hybrid_fwd(Args args) {
;     ...
;             if (r < I_UP) { p0_transpose_item_f8<true>(args.in[15] + (size_t)l * DM * FF, DM, FF, FF / 32, (unsigned char*)(ws + WS_WUP + l * SZ_WUP), WUP8_SCALE, args.in[14] + l * DM, args.in[14] + l * DM, DM, scr, r, lane); continue; } r -= I_UP;
	s_add_i32 s19, s39, 111
	s_min_u32 s19, s19, 127
	s_lshl_b32 s19, s19, 9
	s_add_u32 s12, s46, s19
	s_addc_u32 s13, s47, 0
	global_load_dwordx4 v[132:135], v30, s[12:13]
	s_add_u32 s12, s12, 0x20000
	s_addc_u32 s13, s13, 0
	global_load_dwordx4 v[136:139], v30, s[12:13]
	s_add_u32 s12, s12, 0x20000
	s_addc_u32 s13, s13, 0
	global_load_dwordx4 v[140:143], v30, s[12:13]
	s_add_u32 s12, s12, 0x20000
	s_addc_u32 s13, s13, 0
	global_load_dwordx4 v[144:147], v30, s[12:13]
	s_add_u32 s12, s12, 0x20000
	s_addc_u32 s13, s13, 0
	global_load_dwordx4 v[148:151], v30, s[12:13]
	s_add_u32 s12, s12, 0x20000
	s_addc_u32 s13, s13, 0
	global_load_dwordx4 v[152:155], v30, s[12:13]
	s_add_u32 s12, s12, 0x20000
	s_addc_u32 s13, s13, 0
	global_load_dwordx4 v[156:159], v30, s[12:13]
	s_add_u32 s12, s12, 0x20000
	s_addc_u32 s13, s13, 0
	global_load_dwordx4 v[160:163], v30, s[12:13]
	s_add_i32 s19, s39, 99
	s_min_u32 s19, s19, 127
	s_lshl_b32 s19, s19, 19
	s_add_u32 s14, s64, s19
	s_addc_u32 s15, s65, 0
	ds_read_b32 v170, v7
	ds_read_b32 v171, v7 offset:512
	ds_read_b32 v172, v7 offset:1024
	ds_read_b32 v173, v7 offset:1536
	ds_read_b32 v174, v7 offset:2048
	ds_read_b32 v175, v7 offset:2560
	ds_read_b32 v176, v7 offset:3072
	ds_read_b32 v177, v7 offset:3584
	ds_read_b32 v196, v7 offset:4096
	ds_read_b32 v197, v7 offset:4608
	ds_read_b32 v198, v7 offset:5120
	ds_read_b32 v199, v7 offset:5632
	ds_read_b32 v200, v7 offset:6144
	ds_read_b32 v201, v7 offset:6656
	ds_read_b32 v202, v7 offset:7168
	ds_read_b32 v203, v7 offset:7680
	s_waitcnt lgkmcnt(0)
	v_max_f32_e32 v170, v170, v170
	v_max_f32_e32 v171, v171, v171
	v_max_f32_e32 v172, v172, v172
	v_max_f32_e32 v173, v173, v173
	v_max_f32_e32 v174, v174, v174
	v_max_f32_e32 v175, v175, v175
	v_max_f32_e32 v176, v176, v176
	v_max_f32_e32 v177, v177, v177
	v_max_f32_e32 v196, v196, v196
	v_max_f32_e32 v197, v197, v197
	v_max_f32_e32 v198, v198, v198
	v_max_f32_e32 v199, v199, v199
	v_max_f32_e32 v200, v200, v200
	v_max_f32_e32 v201, v201, v201
	v_max_f32_e32 v202, v202, v202
	v_max_f32_e32 v203, v203, v203
	v_med3_f32 v170, v170, s20, v13
	v_med3_f32 v171, v171, s20, v13
	v_med3_f32 v172, v172, s20, v13
	v_med3_f32 v173, v173, s20, v13
	v_med3_f32 v174, v174, s20, v13
	v_med3_f32 v175, v175, s20, v13
	v_med3_f32 v176, v176, s20, v13
	v_med3_f32 v177, v177, s20, v13
	v_med3_f32 v196, v196, s20, v13
	v_med3_f32 v197, v197, s20, v13
	v_med3_f32 v198, v198, s20, v13
	v_med3_f32 v199, v199, s20, v13
	v_med3_f32 v200, v200, s20, v13
	v_med3_f32 v201, v201, s20, v13
	v_med3_f32 v202, v202, s20, v13
	v_med3_f32 v203, v203, s20, v13
	v_mov_b32_e32 v208, 0
	v_mov_b32_e32 v209, 0
	v_mov_b32_e32 v210, 0
	v_mov_b32_e32 v211, 0
	v_cvt_pk_fp8_f32 v208, v170, v171
	v_cvt_pk_fp8_f32 v209, v174, v175
	v_cvt_pk_fp8_f32 v210, v196, v197
	v_cvt_pk_fp8_f32 v211, v200, v201
	v_cvt_pk_fp8_f32 v208, v172, v173 op_sel:[0,0,1]
	v_cvt_pk_fp8_f32 v209, v176, v177 op_sel:[0,0,1]
	v_cvt_pk_fp8_f32 v210, v198, v199 op_sel:[0,0,1]
	v_cvt_pk_fp8_f32 v211, v202, v203 op_sel:[0,0,1]
	s_nop 0
	global_store_dwordx4 v28, v[208:211], s[14:15]
	ds_read_b32 v170, v9
	ds_read_b32 v171, v9 offset:512
	ds_read_b32 v172, v9 offset:1024
	ds_read_b32 v173, v9 offset:1536
	ds_read_b32 v174, v9 offset:2048
	ds_read_b32 v175, v9 offset:2560
	ds_read_b32 v176, v9 offset:3072
	ds_read_b32 v177, v9 offset:3584
	ds_read_b32 v196, v9 offset:4096
	ds_read_b32 v197, v9 offset:4608
	ds_read_b32 v198, v9 offset:5120
	ds_read_b32 v199, v9 offset:5632
	ds_read_b32 v200, v9 offset:6144
	ds_read_b32 v201, v9 offset:6656
	ds_read_b32 v202, v9 offset:7168
	ds_read_b32 v203, v9 offset:7680
	s_waitcnt lgkmcnt(0)
	v_max_f32_e32 v170, v170, v170
	v_max_f32_e32 v171, v171, v171
	v_max_f32_e32 v172, v172, v172
	v_max_f32_e32 v173, v173, v173
	v_max_f32_e32 v174, v174, v174
	v_max_f32_e32 v175, v175, v175
	v_max_f32_e32 v176, v176, v176
	v_max_f32_e32 v177, v177, v177
	v_max_f32_e32 v196, v196, v196
	v_max_f32_e32 v197, v197, v197
	v_max_f32_e32 v198, v198, v198
	v_max_f32_e32 v199, v199, v199
	v_max_f32_e32 v200, v200, v200
	v_max_f32_e32 v201, v201, v201
	v_max_f32_e32 v202, v202, v202
	v_max_f32_e32 v203, v203, v203
	v_med3_f32 v170, v170, s20, v13
	v_med3_f32 v171, v171, s20, v13
	v_med3_f32 v172, v172, s20, v13
	v_med3_f32 v173, v173, s20, v13
	v_med3_f32 v174, v174, s20, v13
	v_med3_f32 v175, v175, s20, v13
	v_med3_f32 v176, v176, s20, v13
	v_med3_f32 v177, v177, s20, v13
	v_med3_f32 v196, v196, s20, v13
	v_med3_f32 v197, v197, s20, v13
	v_med3_f32 v198, v198, s20, v13
	v_med3_f32 v199, v199, s20, v13
	v_med3_f32 v200, v200, s20, v13
	v_med3_f32 v201, v201, s20, v13
	v_med3_f32 v202, v202, s20, v13
	v_med3_f32 v203, v203, s20, v13
	v_mov_b32_e32 v208, 0
	v_mov_b32_e32 v209, 0
	v_mov_b32_e32 v210, 0
	v_mov_b32_e32 v211, 0
	v_cvt_pk_fp8_f32 v208, v170, v171
	v_cvt_pk_fp8_f32 v209, v174, v175
	v_cvt_pk_fp8_f32 v210, v196, v197
	v_cvt_pk_fp8_f32 v211, v200, v201
	v_cvt_pk_fp8_f32 v208, v172, v173 op_sel:[0,0,1]
	v_cvt_pk_fp8_f32 v209, v176, v177 op_sel:[0,0,1]
	v_cvt_pk_fp8_f32 v210, v198, v199 op_sel:[0,0,1]
	v_cvt_pk_fp8_f32 v211, v202, v203 op_sel:[0,0,1]
	s_nop 0
	global_store_dwordx4 v29, v[208:211], s[14:15]
	s_waitcnt vmcnt(32)
	v_mul_f32_e32 v36, v232, v36
	v_mul_f32_e32 v37, v232, v37
	v_mul_f32_e32 v38, v232, v38
	v_mul_f32_e32 v39, v232, v39
	ds_write_b128 v4, v[36:39]
	v_mul_f32_e32 v40, v233, v40
	v_mul_f32_e32 v41, v233, v41
	v_mul_f32_e32 v42, v233, v42
	v_mul_f32_e32 v43, v233, v43
	ds_write_b128 v4, v[40:43] offset:1024
	v_mul_f32_e32 v44, v234, v44
	v_mul_f32_e32 v45, v234, v45
	v_mul_f32_e32 v46, v234, v46
	v_mul_f32_e32 v47, v234, v47
	ds_write_b128 v4, v[44:47] offset:2048
	v_mul_f32_e32 v48, v235, v48
	v_mul_f32_e32 v49, v235, v49
	v_mul_f32_e32 v50, v235, v50
	v_mul_f32_e32 v51, v235, v51
	ds_write_b128 v4, v[48:51] offset:3072
	v_mul_f32_e32 v52, v236, v52
	v_mul_f32_e32 v53, v236, v53
	v_mul_f32_e32 v54, v236, v54
	v_mul_f32_e32 v55, v236, v55
	ds_write_b128 v4, v[52:55] offset:4096
	v_mul_f32_e32 v56, v237, v56
	v_mul_f32_e32 v57, v237, v57
	v_mul_f32_e32 v58, v237, v58
	v_mul_f32_e32 v59, v237, v59
	ds_write_b128 v4, v[56:59] offset:5120
	v_mul_f32_e32 v60, v238, v60
	v_mul_f32_e32 v61, v238, v61
	v_mul_f32_e32 v62, v238, v62
	v_mul_f32_e32 v63, v238, v63
	ds_write_b128 v4, v[60:63] offset:6144
	v_mul_f32_e32 v64, v239, v64
	v_mul_f32_e32 v65, v239, v65
	v_mul_f32_e32 v66, v239, v66
	v_mul_f32_e32 v67, v239, v67
	ds_write_b128 v4, v[64:67] offset:7168
	s_waitcnt lgkmcnt(0)
	s_barrier
; #define GAS __attribute__((address_space(1)))
; #define LAS __attribute__((address_space(3)))
; #define LDS_WAIT() asm volatile("s_waitcnt lgkmcnt(0)" ::: "memory")
;     ...
; #pragma unroll
;     for (int i = 0; i < 32; ++i) v[i] = sc >= 0 ? W[(size_t)(k0 + 2 * i + (lane >> 5)) * Nsrc + sc] : 0.f;
; #pragma unroll
;     for (int i = 0; i < 32; ++i) { const int k = k0 + 2 * i + (lane >> 5); float x = v[i] * wscale; if (KS) x *= (k < ksplit ? ksA[k] : ksB[k - ksplit]); scr[(2 * i + (lane >> 5)) * 33 + (lane & 31)] = x; }
;     LDS_WAIT(); asm volatile("" ::: "memory");
;     const int c = lane & 7;
; #pragma unroll
;     for (int j = 0; j < 4; ++j) { const int n = (lane >> 3) + 8 * j; const LAS float* s = scr + (8 * c) * 33 + n;
;         const unsigned long long o = (unsigned long long)pg8::pk4_fp8(s[0 * 33], s[1 * 33], s[2 * 33], s[3 * 33]) | ((unsigned long long)pg8::pk4_fp8(s[4 * 33], s[5 * 33], s[6 * 33], s[7 * 33]) << 32);
;         *(GAS unsigned long long*)(WT + (size_t)(n0 + n) * K + k0 + 8 * c) = o; }
;     LDS_WAIT(); asm volatile("" ::: "memory");
	s_add_i32 s19, s39, 114
	s_min_u32 s19, s19, 127
	s_lshl_b32 s19, s19, 9
	s_add_u32 s12, s46, s19
	s_addc_u32 s13, s47, 0
	global_load_dwordx4 v[36:39], v30, s[12:13]
	s_add_u32 s12, s12, 0x20000
	s_addc_u32 s13, s13, 0
	global_load_dwordx4 v[40:43], v30, s[12:13]
	s_add_u32 s12, s12, 0x20000
	s_addc_u32 s13, s13, 0
	global_load_dwordx4 v[44:47], v30, s[12:13]
	s_add_u32 s12, s12, 0x20000
	s_addc_u32 s13, s13, 0
	global_load_dwordx4 v[48:51], v30, s[12:13]
	s_add_u32 s12, s12, 0x20000
	s_addc_u32 s13, s13, 0
	global_load_dwordx4 v[52:55], v30, s[12:13]
	s_add_u32 s12, s12, 0x20000
	s_addc_u32 s13, s13, 0
	global_load_dwordx4 v[56:59], v30, s[12:13]
	s_add_u32 s12, s12, 0x20000
	s_addc_u32 s13, s13, 0
	global_load_dwordx4 v[60:63], v30, s[12:13]
	s_add_u32 s12, s12, 0x20000
	s_addc_u32 s13, s13, 0
	global_load_dwordx4 v[64:67], v30, s[12:13]
	s_add_i32 s19, s39, 102
	s_min_u32 s19, s19, 127
	s_lshl_b32 s19, s19, 19
	s_add_u32 s14, s64, s19
	s_addc_u32 s15, s65, 0
	ds_read_b32 v170, v6
	ds_read_b32 v171, v6 offset:512
	ds_read_b32 v172, v6 offset:1024
	ds_read_b32 v173, v6 offset:1536
	ds_read_b32 v174, v6 offset:2048
	ds_read_b32 v175, v6 offset:2560
	ds_read_b32 v176, v6 offset:3072
	ds_read_b32 v177, v6 offset:3584
	ds_read_b32 v196, v6 offset:4096
	ds_read_b32 v197, v6 offset:4608
	ds_read_b32 v198, v6 offset:5120
	ds_read_b32 v199, v6 offset:5632
	ds_read_b32 v200, v6 offset:6144
	ds_read_b32 v201, v6 offset:6656
	ds_read_b32 v202, v6 offset:7168
	ds_read_b32 v203, v6 offset:7680
	s_waitcnt lgkmcnt(0)
	v_max_f32_e32 v170, v170, v170
	v_max_f32_e32 v171, v171, v171
	v_max_f32_e32 v172, v172, v172
	v_max_f32_e32 v173, v173, v173
	v_max_f32_e32 v174, v174, v174
	v_max_f32_e32 v175, v175, v175
	v_max_f32_e32 v176, v176, v176
	v_max_f32_e32 v177, v177, v177
	v_max_f32_e32 v196, v196, v196
	v_max_f32_e32 v197, v197, v197
	v_max_f32_e32 v198, v198, v198
	v_max_f32_e32 v199, v199, v199
	v_max_f32_e32 v200, v200, v200
	v_max_f32_e32 v201, v201, v201
	v_max_f32_e32 v202, v202, v202
	v_max_f32_e32 v203, v203, v203
	v_med3_f32 v170, v170, s20, v13
	v_med3_f32 v171, v171, s20, v13
	v_med3_f32 v172, v172, s20, v13
	v_med3_f32 v173, v173, s20, v13
	v_med3_f32 v174, v174, s20, v13
	v_med3_f32 v175, v175, s20, v13
	v_med3_f32 v176, v176, s20, v13
	v_med3_f32 v177, v177, s20, v13
	v_med3_f32 v196, v196, s20, v13
	v_med3_f32 v197, v197, s20, v13
	v_med3_f32 v198, v198, s20, v13
	v_med3_f32 v199, v199, s20, v13
	v_med3_f32 v200, v200, s20, v13
	v_med3_f32 v201, v201, s20, v13
	v_med3_f32 v202, v202, s20, v13
	v_med3_f32 v203, v203, s20, v13
	v_mov_b32_e32 v208, 0
	v_mov_b32_e32 v209, 0
	v_mov_b32_e32 v210, 0
	v_mov_b32_e32 v211, 0
	v_cvt_pk_fp8_f32 v208, v170, v171
	v_cvt_pk_fp8_f32 v209, v174, v175
	v_cvt_pk_fp8_f32 v210, v196, v197
	v_cvt_pk_fp8_f32 v211, v200, v201
	v_cvt_pk_fp8_f32 v208, v172, v173 op_sel:[0,0,1]
	v_cvt_pk_fp8_f32 v209, v176, v177 op_sel:[0,0,1]
	v_cvt_pk_fp8_f32 v210, v198, v199 op_sel:[0,0,1]
	v_cvt_pk_fp8_f32 v211, v202, v203 op_sel:[0,0,1]
	s_nop 0
	global_store_dwordx4 v28, v[208:211], s[14:15]
	ds_read_b32 v170, v8
	ds_read_b32 v171, v8 offset:512
	ds_read_b32 v172, v8 offset:1024
	ds_read_b32 v173, v8 offset:1536
	ds_read_b32 v174, v8 offset:2048
	ds_read_b32 v175, v8 offset:2560
	ds_read_b32 v176, v8 offset:3072
	ds_read_b32 v177, v8 offset:3584
	ds_read_b32 v196, v8 offset:4096
	ds_read_b32 v197, v8 offset:4608
	ds_read_b32 v198, v8 offset:5120
	ds_read_b32 v199, v8 offset:5632
	ds_read_b32 v200, v8 offset:6144
	ds_read_b32 v201, v8 offset:6656
	ds_read_b32 v202, v8 offset:7168
	ds_read_b32 v203, v8 offset:7680
	s_waitcnt lgkmcnt(0)
	v_max_f32_e32 v170, v170, v170
	v_max_f32_e32 v171, v171, v171
	v_max_f32_e32 v172, v172, v172
	v_max_f32_e32 v173, v173, v173
	v_max_f32_e32 v174, v174, v174
	v_max_f32_e32 v175, v175, v175
	v_max_f32_e32 v176, v176, v176
	v_max_f32_e32 v177, v177, v177
	v_max_f32_e32 v196, v196, v196
	v_max_f32_e32 v197, v197, v197
	v_max_f32_e32 v198, v198, v198
	v_max_f32_e32 v199, v199, v199
	v_max_f32_e32 v200, v200, v200
	v_max_f32_e32 v201, v201, v201
	v_max_f32_e32 v202, v202, v202
	v_max_f32_e32 v203, v203, v203
	v_med3_f32 v170, v170, s20, v13
	v_med3_f32 v171, v171, s20, v13
	v_med3_f32 v172, v172, s20, v13
	v_med3_f32 v173, v173, s20, v13
	v_med3_f32 v174, v174, s20, v13
	v_med3_f32 v175, v175, s20, v13
	v_med3_f32 v176, v176, s20, v13
	v_med3_f32 v177, v177, s20, v13
	v_med3_f32 v196, v196, s20, v13
	v_med3_f32 v197, v197, s20, v13
	v_med3_f32 v198, v198, s20, v13
	v_med3_f32 v199, v199, s20, v13
	v_med3_f32 v200, v200, s20, v13
	v_med3_f32 v201, v201, s20, v13
	v_med3_f32 v202, v202, s20, v13
	v_med3_f32 v203, v203, s20, v13
	v_mov_b32_e32 v208, 0
	v_mov_b32_e32 v209, 0
	v_mov_b32_e32 v210, 0
	v_mov_b32_e32 v211, 0
	v_cvt_pk_fp8_f32 v208, v170, v171
	v_cvt_pk_fp8_f32 v209, v174, v175
	v_cvt_pk_fp8_f32 v210, v196, v197
	v_cvt_pk_fp8_f32 v211, v200, v201
	v_cvt_pk_fp8_f32 v208, v172, v173 op_sel:[0,0,1]
	v_cvt_pk_fp8_f32 v209, v176, v177 op_sel:[0,0,1]
	v_cvt_pk_fp8_f32 v210, v198, v199 op_sel:[0,0,1]
	v_cvt_pk_fp8_f32 v211, v202, v203 op_sel:[0,0,1]
	s_nop 0
	global_store_dwordx4 v29, v[208:211], s[14:15]
	s_waitcnt vmcnt(32)
	v_mul_f32_e32 v68, v232, v68
	v_mul_f32_e32 v69, v232, v69
	v_mul_f32_e32 v70, v232, v70
	v_mul_f32_e32 v71, v232, v71
	ds_write_b128 v5, v[68:71]
	v_mul_f32_e32 v72, v233, v72
	v_mul_f32_e32 v73, v233, v73
	v_mul_f32_e32 v74, v233, v74
	v_mul_f32_e32 v75, v233, v75
	ds_write_b128 v5, v[72:75] offset:1024
	v_mul_f32_e32 v76, v234, v76
	v_mul_f32_e32 v77, v234, v77
	v_mul_f32_e32 v78, v234, v78
	v_mul_f32_e32 v79, v234, v79
	ds_write_b128 v5, v[76:79] offset:2048
	v_mul_f32_e32 v80, v235, v80
	v_mul_f32_e32 v81, v235, v81
	v_mul_f32_e32 v82, v235, v82
	v_mul_f32_e32 v83, v235, v83
	ds_write_b128 v5, v[80:83] offset:3072
	v_mul_f32_e32 v84, v236, v84
	v_mul_f32_e32 v85, v236, v85
	v_mul_f32_e32 v86, v236, v86
	v_mul_f32_e32 v87, v236, v87
	ds_write_b128 v5, v[84:87] offset:4096
	v_mul_f32_e32 v88, v237, v88
	v_mul_f32_e32 v89, v237, v89
	v_mul_f32_e32 v90, v237, v90
	v_mul_f32_e32 v91, v237, v91
	ds_write_b128 v5, v[88:91] offset:5120
	v_mul_f32_e32 v92, v238, v92
	v_mul_f32_e32 v93, v238, v93
	v_mul_f32_e32 v94, v238, v94
	v_mul_f32_e32 v95, v238, v95
	ds_write_b128 v5, v[92:95] offset:6144
	v_mul_f32_e32 v96, v239, v96
	v_mul_f32_e32 v97, v239, v97
	v_mul_f32_e32 v98, v239, v98
	v_mul_f32_e32 v99, v239, v99
	ds_write_b128 v5, v[96:99] offset:7168
	s_waitcnt lgkmcnt(0)
	s_barrier
; #define GAS __attribute__((address_space(1)))
; #define LAS __attribute__((address_space(3)))
; #define LDS_WAIT() asm volatile("s_waitcnt lgkmcnt(0)" ::: "memory")
;     ...
; #pragma unroll
;     for (int i = 0; i < 32; ++i) v[i] = sc >= 0 ? W[(size_t)(k0 + 2 * i + (lane >> 5)) * Nsrc + sc] : 0.f;
; #pragma unroll
;     for (int i = 0; i < 32; ++i) { const int k = k0 + 2 * i + (lane >> 5); float x = v[i] * wscale; if (KS) x *= (k < ksplit ? ksA[k] : ksB[k - ksplit]); scr[(2 * i + (lane >> 5)) * 33 + (lane & 31)] = x; }
;     LDS_WAIT(); asm volatile("" ::: "memory");
;     const int c = lane & 7;
; #pragma unroll
;     for (int j = 0; j < 4; ++j) { const int n = (lane >> 3) + 8 * j; const LAS float* s = scr + (8 * c) * 33 + n;
;         const unsigned long long o = (unsigned long long)pg8::pk4_fp8(s[0 * 33], s[1 * 33], s[2 * 33], s[3 * 33]) | ((unsigned long long)pg8::pk4_fp8(s[4 * 33], s[5 * 33], s[6 * 33], s[7 * 33]) << 32);
;         *(GAS unsigned long long*)(WT + (size_t)(n0 + n) * K + k0 + 8 * c) = o; }
;     LDS_WAIT(); asm volatile("" ::: "memory");
	s_add_i32 s19, s39, 117
	s_min_u32 s19, s19, 127
	s_lshl_b32 s19, s19, 9
	s_add_u32 s12, s46, s19
	s_addc_u32 s13, s47, 0
	global_load_dwordx4 v[68:71], v30, s[12:13]
	s_add_u32 s12, s12, 0x20000
	s_addc_u32 s13, s13, 0
	global_load_dwordx4 v[72:75], v30, s[12:13]
	s_add_u32 s12, s12, 0x20000
	s_addc_u32 s13, s13, 0
	global_load_dwordx4 v[76:79], v30, s[12:13]
	s_add_u32 s12, s12, 0x20000
	s_addc_u32 s13, s13, 0
	global_load_dwordx4 v[80:83], v30, s[12:13]
	s_add_u32 s12, s12, 0x20000
	s_addc_u32 s13, s13, 0
	global_load_dwordx4 v[84:87], v30, s[12:13]
	s_add_u32 s12, s12, 0x20000
	s_addc_u32 s13, s13, 0
	global_load_dwordx4 v[88:91], v30, s[12:13]
	s_add_u32 s12, s12, 0x20000
	s_addc_u32 s13, s13, 0
	global_load_dwordx4 v[92:95], v30, s[12:13]
	s_add_u32 s12, s12, 0x20000
	s_addc_u32 s13, s13, 0
	global_load_dwordx4 v[96:99], v30, s[12:13]
	s_add_i32 s19, s39, 105
	s_min_u32 s19, s19, 127
	s_lshl_b32 s19, s19, 19
	s_add_u32 s14, s64, s19
	s_addc_u32 s15, s65, 0
	ds_read_b32 v170, v7
	ds_read_b32 v171, v7 offset:512
	ds_read_b32 v172, v7 offset:1024
	ds_read_b32 v173, v7 offset:1536
	ds_read_b32 v174, v7 offset:2048
	ds_read_b32 v175, v7 offset:2560
	ds_read_b32 v176, v7 offset:3072
	ds_read_b32 v177, v7 offset:3584
	ds_read_b32 v196, v7 offset:4096
	ds_read_b32 v197, v7 offset:4608
	ds_read_b32 v198, v7 offset:5120
	ds_read_b32 v199, v7 offset:5632
	ds_read_b32 v200, v7 offset:6144
	ds_read_b32 v201, v7 offset:6656
	ds_read_b32 v202, v7 offset:7168
	ds_read_b32 v203, v7 offset:7680
	s_waitcnt lgkmcnt(0)
	v_max_f32_e32 v170, v170, v170
	v_max_f32_e32 v171, v171, v171
	v_max_f32_e32 v172, v172, v172
	v_max_f32_e32 v173, v173, v173
	v_max_f32_e32 v174, v174, v174
	v_max_f32_e32 v175, v175, v175
	v_max_f32_e32 v176, v176, v176
	v_max_f32_e32 v177, v177, v177
	v_max_f32_e32 v196, v196, v196
	v_max_f32_e32 v197, v197, v197
	v_max_f32_e32 v198, v198, v198
	v_max_f32_e32 v199, v199, v199
	v_max_f32_e32 v200, v200, v200
	v_max_f32_e32 v201, v201, v201
	v_max_f32_e32 v202, v202, v202
	v_max_f32_e32 v203, v203, v203
	v_med3_f32 v170, v170, s20, v13
	v_med3_f32 v171, v171, s20, v13
	v_med3_f32 v172, v172, s20, v13
	v_med3_f32 v173, v173, s20, v13
	v_med3_f32 v174, v174, s20, v13
	v_med3_f32 v175, v175, s20, v13
	v_med3_f32 v176, v176, s20, v13
	v_med3_f32 v177, v177, s20, v13
	v_med3_f32 v196, v196, s20, v13
	v_med3_f32 v197, v197, s20, v13
	v_med3_f32 v198, v198, s20, v13
	v_med3_f32 v199, v199, s20, v13
	v_med3_f32 v200, v200, s20, v13
	v_med3_f32 v201, v201, s20, v13
	v_med3_f32 v202, v202, s20, v13
	v_med3_f32 v203, v203, s20, v13
	v_mov_b32_e32 v208, 0
	v_mov_b32_e32 v209, 0
	v_mov_b32_e32 v210, 0
	v_mov_b32_e32 v211, 0
	v_cvt_pk_fp8_f32 v208, v170, v171
	v_cvt_pk_fp8_f32 v209, v174, v175
	v_cvt_pk_fp8_f32 v210, v196, v197
	v_cvt_pk_fp8_f32 v211, v200, v201
	v_cvt_pk_fp8_f32 v208, v172, v173 op_sel:[0,0,1]
	v_cvt_pk_fp8_f32 v209, v176, v177 op_sel:[0,0,1]
	v_cvt_pk_fp8_f32 v210, v198, v199 op_sel:[0,0,1]
	v_cvt_pk_fp8_f32 v211, v202, v203 op_sel:[0,0,1]
	s_nop 0
	global_store_dwordx4 v28, v[208:211], s[14:15]
	ds_read_b32 v170, v9
	ds_read_b32 v171, v9 offset:512
	ds_read_b32 v172, v9 offset:1024
	ds_read_b32 v173, v9 offset:1536
	ds_read_b32 v174, v9 offset:2048
	ds_read_b32 v175, v9 offset:2560
	ds_read_b32 v176, v9 offset:3072
	ds_read_b32 v177, v9 offset:3584
	ds_read_b32 v196, v9 offset:4096
	ds_read_b32 v197, v9 offset:4608
	ds_read_b32 v198, v9 offset:5120
	ds_read_b32 v199, v9 offset:5632
	ds_read_b32 v200, v9 offset:6144
	ds_read_b32 v201, v9 offset:6656
	ds_read_b32 v202, v9 offset:7168
	ds_read_b32 v203, v9 offset:7680
	s_waitcnt lgkmcnt(0)
	v_max_f32_e32 v170, v170, v170
	v_max_f32_e32 v171, v171, v171
	v_max_f32_e32 v172, v172, v172
	v_max_f32_e32 v173, v173, v173
	v_max_f32_e32 v174, v174, v174
	v_max_f32_e32 v175, v175, v175
	v_max_f32_e32 v176, v176, v176
	v_max_f32_e32 v177, v177, v177
	v_max_f32_e32 v196, v196, v196
	v_max_f32_e32 v197, v197, v197
	v_max_f32_e32 v198, v198, v198
	v_max_f32_e32 v199, v199, v199
	v_max_f32_e32 v200, v200, v200
	v_max_f32_e32 v201, v201, v201
	v_max_f32_e32 v202, v202, v202
	v_max_f32_e32 v203, v203, v203
	v_med3_f32 v170, v170, s20, v13
	v_med3_f32 v171, v171, s20, v13
	v_med3_f32 v172, v172, s20, v13
	v_med3_f32 v173, v173, s20, v13
	v_med3_f32 v174, v174, s20, v13
	v_med3_f32 v175, v175, s20, v13
	v_med3_f32 v176, v176, s20, v13
	v_med3_f32 v177, v177, s20, v13
	v_med3_f32 v196, v196, s20, v13
	v_med3_f32 v197, v197, s20, v13
	v_med3_f32 v198, v198, s20, v13
	v_med3_f32 v199, v199, s20, v13
	v_med3_f32 v200, v200, s20, v13
	v_med3_f32 v201, v201, s20, v13
	v_med3_f32 v202, v202, s20, v13
	v_med3_f32 v203, v203, s20, v13
	v_mov_b32_e32 v208, 0
	v_mov_b32_e32 v209, 0
	v_mov_b32_e32 v210, 0
	v_mov_b32_e32 v211, 0
	v_cvt_pk_fp8_f32 v208, v170, v171
	v_cvt_pk_fp8_f32 v209, v174, v175
	v_cvt_pk_fp8_f32 v210, v196, v197
	v_cvt_pk_fp8_f32 v211, v200, v201
	v_cvt_pk_fp8_f32 v208, v172, v173 op_sel:[0,0,1]
	v_cvt_pk_fp8_f32 v209, v176, v177 op_sel:[0,0,1]
	v_cvt_pk_fp8_f32 v210, v198, v199 op_sel:[0,0,1]
	v_cvt_pk_fp8_f32 v211, v202, v203 op_sel:[0,0,1]
	s_nop 0
	global_store_dwordx4 v29, v[208:211], s[14:15]
	s_waitcnt vmcnt(32)
	v_mul_f32_e32 v100, v232, v100
	v_mul_f32_e32 v101, v232, v101
	v_mul_f32_e32 v102, v232, v102
	v_mul_f32_e32 v103, v232, v103
	ds_write_b128 v4, v[100:103]
	v_mul_f32_e32 v104, v233, v104
	v_mul_f32_e32 v105, v233, v105
	v_mul_f32_e32 v106, v233, v106
	v_mul_f32_e32 v107, v233, v107
	ds_write_b128 v4, v[104:107] offset:1024
	v_mul_f32_e32 v108, v234, v108
	v_mul_f32_e32 v109, v234, v109
	v_mul_f32_e32 v110, v234, v110
	v_mul_f32_e32 v111, v234, v111
	ds_write_b128 v4, v[108:111] offset:2048
	v_mul_f32_e32 v112, v235, v112
	v_mul_f32_e32 v113, v235, v113
	v_mul_f32_e32 v114, v235, v114
	v_mul_f32_e32 v115, v235, v115
	ds_write_b128 v4, v[112:115] offset:3072
	v_mul_f32_e32 v116, v236, v116
	v_mul_f32_e32 v117, v236, v117
	v_mul_f32_e32 v118, v236, v118
	v_mul_f32_e32 v119, v236, v119
	ds_write_b128 v4, v[116:119] offset:4096
	v_mul_f32_e32 v120, v237, v120
	v_mul_f32_e32 v121, v237, v121
	v_mul_f32_e32 v122, v237, v122
	v_mul_f32_e32 v123, v237, v123
	ds_write_b128 v4, v[120:123] offset:5120
	v_mul_f32_e32 v124, v238, v124
	v_mul_f32_e32 v125, v238, v125
	v_mul_f32_e32 v126, v238, v126
	v_mul_f32_e32 v127, v238, v127
	ds_write_b128 v4, v[124:127] offset:6144
	v_mul_f32_e32 v128, v239, v128
	v_mul_f32_e32 v129, v239, v129
	v_mul_f32_e32 v130, v239, v130
	v_mul_f32_e32 v131, v239, v131
	ds_write_b128 v4, v[128:131] offset:7168
	s_waitcnt lgkmcnt(0)
	s_barrier
; #define GAS __attribute__((address_space(1)))
; #define LAS __attribute__((address_space(3)))
; #define LDS_WAIT() asm volatile("s_waitcnt lgkmcnt(0)" ::: "memory")
;     ...
; #pragma unroll
;     for (int i = 0; i < 32; ++i) v[i] = sc >= 0 ? W[(size_t)(k0 + 2 * i + (lane >> 5)) * Nsrc + sc] : 0.f;
; #pragma unroll
;     for (int i = 0; i < 32; ++i) { const int k = k0 + 2 * i + (lane >> 5); float x = v[i] * wscale; if (KS) x *= (k < ksplit ? ksA[k] : ksB[k - ksplit]); scr[(2 * i + (lane >> 5)) * 33 + (lane & 31)] = x; }
;     LDS_WAIT(); asm volatile("" ::: "memory");
;     const int c = lane & 7;
; #pragma unroll
;     for (int j = 0; j < 4; ++j) { const int n = (lane >> 3) + 8 * j; const LAS float* s = scr + (8 * c) * 33 + n;
;         const unsigned long long o = (unsigned long long)pg8::pk4_fp8(s[0 * 33], s[1 * 33], s[2 * 33], s[3 * 33]) | ((unsigned long long)pg8::pk4_fp8(s[4 * 33], s[5 * 33], s[6 * 33], s[7 * 33]) << 32);
;         *(GAS unsigned long long*)(WT + (size_t)(n0 + n) * K + k0 + 8 * c) = o; }
;     LDS_WAIT(); asm volatile("" ::: "memory");
	s_add_i32 s19, s39, 120
	s_min_u32 s19, s19, 127
	s_lshl_b32 s19, s19, 9
	s_add_u32 s12, s46, s19
	s_addc_u32 s13, s47, 0
	global_load_dwordx4 v[100:103], v30, s[12:13]
	s_add_u32 s12, s12, 0x20000
	s_addc_u32 s13, s13, 0
	global_load_dwordx4 v[104:107], v30, s[12:13]
	s_add_u32 s12, s12, 0x20000
	s_addc_u32 s13, s13, 0
	global_load_dwordx4 v[108:111], v30, s[12:13]
	s_add_u32 s12, s12, 0x20000
	s_addc_u32 s13, s13, 0
	global_load_dwordx4 v[112:115], v30, s[12:13]
	s_add_u32 s12, s12, 0x20000
	s_addc_u32 s13, s13, 0
	global_load_dwordx4 v[116:119], v30, s[12:13]
	s_add_u32 s12, s12, 0x20000
	s_addc_u32 s13, s13, 0
	global_load_dwordx4 v[120:123], v30, s[12:13]
	s_add_u32 s12, s12, 0x20000
	s_addc_u32 s13, s13, 0
	global_load_dwordx4 v[124:127], v30, s[12:13]
	s_add_u32 s12, s12, 0x20000
	s_addc_u32 s13, s13, 0
	global_load_dwordx4 v[128:131], v30, s[12:13]
	s_add_i32 s19, s39, 108
	s_min_u32 s19, s19, 127
	s_lshl_b32 s19, s19, 19
	s_add_u32 s14, s64, s19
	s_addc_u32 s15, s65, 0
	ds_read_b32 v170, v6
	ds_read_b32 v171, v6 offset:512
	ds_read_b32 v172, v6 offset:1024
	ds_read_b32 v173, v6 offset:1536
	ds_read_b32 v174, v6 offset:2048
	ds_read_b32 v175, v6 offset:2560
	ds_read_b32 v176, v6 offset:3072
	ds_read_b32 v177, v6 offset:3584
	ds_read_b32 v196, v6 offset:4096
	ds_read_b32 v197, v6 offset:4608
	ds_read_b32 v198, v6 offset:5120
	ds_read_b32 v199, v6 offset:5632
	ds_read_b32 v200, v6 offset:6144
	ds_read_b32 v201, v6 offset:6656
	ds_read_b32 v202, v6 offset:7168
	ds_read_b32 v203, v6 offset:7680
	s_waitcnt lgkmcnt(0)
	v_max_f32_e32 v170, v170, v170
	v_max_f32_e32 v171, v171, v171
	v_max_f32_e32 v172, v172, v172
	v_max_f32_e32 v173, v173, v173
	v_max_f32_e32 v174, v174, v174
	v_max_f32_e32 v175, v175, v175
	v_max_f32_e32 v176, v176, v176
	v_max_f32_e32 v177, v177, v177
	v_max_f32_e32 v196, v196, v196
	v_max_f32_e32 v197, v197, v197
	v_max_f32_e32 v198, v198, v198
	v_max_f32_e32 v199, v199, v199
	v_max_f32_e32 v200, v200, v200
	v_max_f32_e32 v201, v201, v201
	v_max_f32_e32 v202, v202, v202
	v_max_f32_e32 v203, v203, v203
	v_med3_f32 v170, v170, s20, v13
	v_med3_f32 v171, v171, s20, v13
	v_med3_f32 v172, v172, s20, v13
	v_med3_f32 v173, v173, s20, v13
	v_med3_f32 v174, v174, s20, v13
	v_med3_f32 v175, v175, s20, v13
	v_med3_f32 v176, v176, s20, v13
	v_med3_f32 v177, v177, s20, v13
	v_med3_f32 v196, v196, s20, v13
	v_med3_f32 v197, v197, s20, v13
	v_med3_f32 v198, v198, s20, v13
	v_med3_f32 v199, v199, s20, v13
	v_med3_f32 v200, v200, s20, v13
	v_med3_f32 v201, v201, s20, v13
	v_med3_f32 v202, v202, s20, v13
	v_med3_f32 v203, v203, s20, v13
	v_mov_b32_e32 v208, 0
	v_mov_b32_e32 v209, 0
	v_mov_b32_e32 v210, 0
	v_mov_b32_e32 v211, 0
	v_cvt_pk_fp8_f32 v208, v170, v171
	v_cvt_pk_fp8_f32 v209, v174, v175
	v_cvt_pk_fp8_f32 v210, v196, v197
	v_cvt_pk_fp8_f32 v211, v200, v201
	v_cvt_pk_fp8_f32 v208, v172, v173 op_sel:[0,0,1]
	v_cvt_pk_fp8_f32 v209, v176, v177 op_sel:[0,0,1]
	v_cvt_pk_fp8_f32 v210, v198, v199 op_sel:[0,0,1]
	v_cvt_pk_fp8_f32 v211, v202, v203 op_sel:[0,0,1]
	s_nop 0
	global_store_dwordx4 v28, v[208:211], s[14:15]
	ds_read_b32 v170, v8
	ds_read_b32 v171, v8 offset:512
	ds_read_b32 v172, v8 offset:1024
	ds_read_b32 v173, v8 offset:1536
	ds_read_b32 v174, v8 offset:2048
	ds_read_b32 v175, v8 offset:2560
	ds_read_b32 v176, v8 offset:3072
	ds_read_b32 v177, v8 offset:3584
	ds_read_b32 v196, v8 offset:4096
	ds_read_b32 v197, v8 offset:4608
	ds_read_b32 v198, v8 offset:5120
	ds_read_b32 v199, v8 offset:5632
	ds_read_b32 v200, v8 offset:6144
	ds_read_b32 v201, v8 offset:6656
	ds_read_b32 v202, v8 offset:7168
	ds_read_b32 v203, v8 offset:7680
	s_waitcnt lgkmcnt(0)
	v_max_f32_e32 v170, v170, v170
	v_max_f32_e32 v171, v171, v171
	v_max_f32_e32 v172, v172, v172
	v_max_f32_e32 v173, v173, v173
	v_max_f32_e32 v174, v174, v174
	v_max_f32_e32 v175, v175, v175
	v_max_f32_e32 v176, v176, v176
	v_max_f32_e32 v177, v177, v177
	v_max_f32_e32 v196, v196, v196
	v_max_f32_e32 v197, v197, v197
	v_max_f32_e32 v198, v198, v198
	v_max_f32_e32 v199, v199, v199
	v_max_f32_e32 v200, v200, v200
	v_max_f32_e32 v201, v201, v201
	v_max_f32_e32 v202, v202, v202
	v_max_f32_e32 v203, v203, v203
	v_med3_f32 v170, v170, s20, v13
	v_med3_f32 v171, v171, s20, v13
	v_med3_f32 v172, v172, s20, v13
	v_med3_f32 v173, v173, s20, v13
	v_med3_f32 v174, v174, s20, v13
	v_med3_f32 v175, v175, s20, v13
	v_med3_f32 v176, v176, s20, v13
	v_med3_f32 v177, v177, s20, v13
	v_med3_f32 v196, v196, s20, v13
	v_med3_f32 v197, v197, s20, v13
	v_med3_f32 v198, v198, s20, v13
	v_med3_f32 v199, v199, s20, v13
	v_med3_f32 v200, v200, s20, v13
	v_med3_f32 v201, v201, s20, v13
	v_med3_f32 v202, v202, s20, v13
	v_med3_f32 v203, v203, s20, v13
	v_mov_b32_e32 v208, 0
	v_mov_b32_e32 v209, 0
	v_mov_b32_e32 v210, 0
	v_mov_b32_e32 v211, 0
	v_cvt_pk_fp8_f32 v208, v170, v171
	v_cvt_pk_fp8_f32 v209, v174, v175
	v_cvt_pk_fp8_f32 v210, v196, v197
	v_cvt_pk_fp8_f32 v211, v200, v201
	v_cvt_pk_fp8_f32 v208, v172, v173 op_sel:[0,0,1]
	v_cvt_pk_fp8_f32 v209, v176, v177 op_sel:[0,0,1]
	v_cvt_pk_fp8_f32 v210, v198, v199 op_sel:[0,0,1]
	v_cvt_pk_fp8_f32 v211, v202, v203 op_sel:[0,0,1]
	s_nop 0
	global_store_dwordx4 v29, v[208:211], s[14:15]
	s_waitcnt vmcnt(32)
	v_mul_f32_e32 v132, v232, v132
	v_mul_f32_e32 v133, v232, v133
	v_mul_f32_e32 v134, v232, v134
	v_mul_f32_e32 v135, v232, v135
	ds_write_b128 v5, v[132:135]
	v_mul_f32_e32 v136, v233, v136
	v_mul_f32_e32 v137, v233, v137
	v_mul_f32_e32 v138, v233, v138
	v_mul_f32_e32 v139, v233, v139
	ds_write_b128 v5, v[136:139] offset:1024
	v_mul_f32_e32 v140, v234, v140
	v_mul_f32_e32 v141, v234, v141
	v_mul_f32_e32 v142, v234, v142
	v_mul_f32_e32 v143, v234, v143
	ds_write_b128 v5, v[140:143] offset:2048
	v_mul_f32_e32 v144, v235, v144
	v_mul_f32_e32 v145, v235, v145
	v_mul_f32_e32 v146, v235, v146
	v_mul_f32_e32 v147, v235, v147
	ds_write_b128 v5, v[144:147] offset:3072
	v_mul_f32_e32 v148, v236, v148
	v_mul_f32_e32 v149, v236, v149
	v_mul_f32_e32 v150, v236, v150
	v_mul_f32_e32 v151, v236, v151
	ds_write_b128 v5, v[148:151] offset:4096
	v_mul_f32_e32 v152, v237, v152
	v_mul_f32_e32 v153, v237, v153
	v_mul_f32_e32 v154, v237, v154
	v_mul_f32_e32 v155, v237, v155
	ds_write_b128 v5, v[152:155] offset:5120
	v_mul_f32_e32 v156, v238, v156
	v_mul_f32_e32 v157, v238, v157
	v_mul_f32_e32 v158, v238, v158
	v_mul_f32_e32 v159, v238, v159
	ds_write_b128 v5, v[156:159] offset:6144
	v_mul_f32_e32 v160, v239, v160
	v_mul_f32_e32 v161, v239, v161
	v_mul_f32_e32 v162, v239, v162
	v_mul_f32_e32 v163, v239, v163
	ds_write_b128 v5, v[160:163] offset:7168
	s_waitcnt lgkmcnt(0)
	s_barrier
; #define GAS __attribute__((address_space(1)))
; #define LAS __attribute__((address_space(3)))
; #define LDS_WAIT() asm volatile("s_waitcnt lgkmcnt(0)" ::: "memory")
;     ...
; #pragma unroll
;     for (int i = 0; i < 32; ++i) v[i] = sc >= 0 ? W[(size_t)(k0 + 2 * i + (lane >> 5)) * Nsrc + sc] : 0.f;
; #pragma unroll
;     for (int i = 0; i < 32; ++i) { const int k = k0 + 2 * i + (lane >> 5); float x = v[i] * wscale; if (KS) x *= (k < ksplit ? ksA[k] : ksB[k - ksplit]); scr[(2 * i + (lane >> 5)) * 33 + (lane & 31)] = x; }
;     LDS_WAIT(); asm volatile("" ::: "memory");
;     const int c = lane & 7;
; #pragma unroll
;     for (int j = 0; j < 4; ++j) { const int n = (lane >> 3) + 8 * j; const LAS float* s = scr + (8 * c) * 33 + n;
;         const unsigned long long o = (unsigned long long)pg8::pk4_fp8(s[0 * 33], s[1 * 33], s[2 * 33], s[3 * 33]) | ((unsigned long long)pg8::pk4_fp8(s[4 * 33], s[5 * 33], s[6 * 33], s[7 * 33]) << 32);
;         *(GAS unsigned long long*)(WT + (size_t)(n0 + n) * K + k0 + 8 * c) = o; }
;     LDS_WAIT(); asm volatile("" ::: "memory");
	s_add_i32 s19, s39, 123
	s_min_u32 s19, s19, 127
	s_lshl_b32 s19, s19, 9
	s_add_u32 s12, s46, s19
	s_addc_u32 s13, s47, 0
	global_load_dwordx4 v[132:135], v30, s[12:13]
	s_add_u32 s12, s12, 0x20000
	s_addc_u32 s13, s13, 0
	global_load_dwordx4 v[136:139], v30, s[12:13]
	s_add_u32 s12, s12, 0x20000
	s_addc_u32 s13, s13, 0
	global_load_dwordx4 v[140:143], v30, s[12:13]
	s_add_u32 s12, s12, 0x20000
	s_addc_u32 s13, s13, 0
	global_load_dwordx4 v[144:147], v30, s[12:13]
	s_add_u32 s12, s12, 0x20000
	s_addc_u32 s13, s13, 0
	global_load_dwordx4 v[148:151], v30, s[12:13]
	s_add_u32 s12, s12, 0x20000
	s_addc_u32 s13, s13, 0
	global_load_dwordx4 v[152:155], v30, s[12:13]
	s_add_u32 s12, s12, 0x20000
	s_addc_u32 s13, s13, 0
	global_load_dwordx4 v[156:159], v30, s[12:13]
	s_add_u32 s12, s12, 0x20000
	s_addc_u32 s13, s13, 0
	global_load_dwordx4 v[160:163], v30, s[12:13]
	s_add_i32 s19, s39, 111
	s_min_u32 s19, s19, 127
	s_lshl_b32 s19, s19, 19
	s_add_u32 s14, s64, s19
	s_addc_u32 s15, s65, 0
	ds_read_b32 v170, v7
	ds_read_b32 v171, v7 offset:512
	ds_read_b32 v172, v7 offset:1024
	ds_read_b32 v173, v7 offset:1536
	ds_read_b32 v174, v7 offset:2048
	ds_read_b32 v175, v7 offset:2560
	ds_read_b32 v176, v7 offset:3072
	ds_read_b32 v177, v7 offset:3584
	ds_read_b32 v196, v7 offset:4096
	ds_read_b32 v197, v7 offset:4608
	ds_read_b32 v198, v7 offset:5120
	ds_read_b32 v199, v7 offset:5632
	ds_read_b32 v200, v7 offset:6144
	ds_read_b32 v201, v7 offset:6656
	ds_read_b32 v202, v7 offset:7168
	ds_read_b32 v203, v7 offset:7680
	s_waitcnt lgkmcnt(0)
	v_max_f32_e32 v170, v170, v170
	v_max_f32_e32 v171, v171, v171
	v_max_f32_e32 v172, v172, v172
	v_max_f32_e32 v173, v173, v173
	v_max_f32_e32 v174, v174, v174
	v_max_f32_e32 v175, v175, v175
	v_max_f32_e32 v176, v176, v176
	v_max_f32_e32 v177, v177, v177
	v_max_f32_e32 v196, v196, v196
	v_max_f32_e32 v197, v197, v197
	v_max_f32_e32 v198, v198, v198
	v_max_f32_e32 v199, v199, v199
	v_max_f32_e32 v200, v200, v200
	v_max_f32_e32 v201, v201, v201
	v_max_f32_e32 v202, v202, v202
	v_max_f32_e32 v203, v203, v203
	v_med3_f32 v170, v170, s20, v13
	v_med3_f32 v171, v171, s20, v13
	v_med3_f32 v172, v172, s20, v13
	v_med3_f32 v173, v173, s20, v13
	v_med3_f32 v174, v174, s20, v13
	v_med3_f32 v175, v175, s20, v13
	v_med3_f32 v176, v176, s20, v13
	v_med3_f32 v177, v177, s20, v13
	v_med3_f32 v196, v196, s20, v13
	v_med3_f32 v197, v197, s20, v13
	v_med3_f32 v198, v198, s20, v13
	v_med3_f32 v199, v199, s20, v13
	v_med3_f32 v200, v200, s20, v13
	v_med3_f32 v201, v201, s20, v13
	v_med3_f32 v202, v202, s20, v13
	v_med3_f32 v203, v203, s20, v13
	v_mov_b32_e32 v208, 0
	v_mov_b32_e32 v209, 0
	v_mov_b32_e32 v210, 0
	v_mov_b32_e32 v211, 0
	v_cvt_pk_fp8_f32 v208, v170, v171
	v_cvt_pk_fp8_f32 v209, v174, v175
	v_cvt_pk_fp8_f32 v210, v196, v197
	v_cvt_pk_fp8_f32 v211, v200, v201
	v_cvt_pk_fp8_f32 v208, v172, v173 op_sel:[0,0,1]
	v_cvt_pk_fp8_f32 v209, v176, v177 op_sel:[0,0,1]
	v_cvt_pk_fp8_f32 v210, v198, v199 op_sel:[0,0,1]
	v_cvt_pk_fp8_f32 v211, v202, v203 op_sel:[0,0,1]
	s_nop 0
	global_store_dwordx4 v28, v[208:211], s[14:15]
	ds_read_b32 v170, v9
	ds_read_b32 v171, v9 offset:512
	ds_read_b32 v172, v9 offset:1024
	ds_read_b32 v173, v9 offset:1536
	ds_read_b32 v174, v9 offset:2048
	ds_read_b32 v175, v9 offset:2560
	ds_read_b32 v176, v9 offset:3072
	ds_read_b32 v177, v9 offset:3584
	ds_read_b32 v196, v9 offset:4096
	ds_read_b32 v197, v9 offset:4608
	ds_read_b32 v198, v9 offset:5120
	ds_read_b32 v199, v9 offset:5632
	ds_read_b32 v200, v9 offset:6144
	ds_read_b32 v201, v9 offset:6656
	ds_read_b32 v202, v9 offset:7168
	ds_read_b32 v203, v9 offset:7680
	s_waitcnt lgkmcnt(0)
	v_max_f32_e32 v170, v170, v170
	v_max_f32_e32 v171, v171, v171
	v_max_f32_e32 v172, v172, v172
	v_max_f32_e32 v173, v173, v173
	v_max_f32_e32 v174, v174, v174
	v_max_f32_e32 v175, v175, v175
	v_max_f32_e32 v176, v176, v176
	v_max_f32_e32 v177, v177, v177
	v_max_f32_e32 v196, v196, v196
	v_max_f32_e32 v197, v197, v197
	v_max_f32_e32 v198, v198, v198
	v_max_f32_e32 v199, v199, v199
	v_max_f32_e32 v200, v200, v200
	v_max_f32_e32 v201, v201, v201
	v_max_f32_e32 v202, v202, v202
	v_max_f32_e32 v203, v203, v203
	v_med3_f32 v170, v170, s20, v13
	v_med3_f32 v171, v171, s20, v13
	v_med3_f32 v172, v172, s20, v13
	v_med3_f32 v173, v173, s20, v13
	v_med3_f32 v174, v174, s20, v13
	v_med3_f32 v175, v175, s20, v13
	v_med3_f32 v176, v176, s20, v13
	v_med3_f32 v177, v177, s20, v13
	v_med3_f32 v196, v196, s20, v13
	v_med3_f32 v197, v197, s20, v13
	v_med3_f32 v198, v198, s20, v13
	v_med3_f32 v199, v199, s20, v13
	v_med3_f32 v200, v200, s20, v13
	v_med3_f32 v201, v201, s20, v13
	v_med3_f32 v202, v202, s20, v13
	v_med3_f32 v203, v203, s20, v13
	v_mov_b32_e32 v208, 0
	v_mov_b32_e32 v209, 0
	v_mov_b32_e32 v210, 0
	v_mov_b32_e32 v211, 0
	v_cvt_pk_fp8_f32 v208, v170, v171
	v_cvt_pk_fp8_f32 v209, v174, v175
	v_cvt_pk_fp8_f32 v210, v196, v197
	v_cvt_pk_fp8_f32 v211, v200, v201
	v_cvt_pk_fp8_f32 v208, v172, v173 op_sel:[0,0,1]
	v_cvt_pk_fp8_f32 v209, v176, v177 op_sel:[0,0,1]
	v_cvt_pk_fp8_f32 v210, v198, v199 op_sel:[0,0,1]
	v_cvt_pk_fp8_f32 v211, v202, v203 op_sel:[0,0,1]
	s_nop 0
	global_store_dwordx4 v29, v[208:211], s[14:15]
	s_waitcnt vmcnt(32)
	v_mul_f32_e32 v36, v232, v36
	v_mul_f32_e32 v37, v232, v37
	v_mul_f32_e32 v38, v232, v38
	v_mul_f32_e32 v39, v232, v39
	ds_write_b128 v4, v[36:39]
	v_mul_f32_e32 v40, v233, v40
	v_mul_f32_e32 v41, v233, v41
	v_mul_f32_e32 v42, v233, v42
	v_mul_f32_e32 v43, v233, v43
	ds_write_b128 v4, v[40:43] offset:1024
	v_mul_f32_e32 v44, v234, v44
	v_mul_f32_e32 v45, v234, v45
	v_mul_f32_e32 v46, v234, v46
	v_mul_f32_e32 v47, v234, v47
	ds_write_b128 v4, v[44:47] offset:2048
	v_mul_f32_e32 v48, v235, v48
	v_mul_f32_e32 v49, v235, v49
	v_mul_f32_e32 v50, v235, v50
	v_mul_f32_e32 v51, v235, v51
	ds_write_b128 v4, v[48:51] offset:3072
	v_mul_f32_e32 v52, v236, v52
	v_mul_f32_e32 v53, v236, v53
	v_mul_f32_e32 v54, v236, v54
	v_mul_f32_e32 v55, v236, v55
	ds_write_b128 v4, v[52:55] offset:4096
	v_mul_f32_e32 v56, v237, v56
	v_mul_f32_e32 v57, v237, v57
	v_mul_f32_e32 v58, v237, v58
	v_mul_f32_e32 v59, v237, v59
	ds_write_b128 v4, v[56:59] offset:5120
	v_mul_f32_e32 v60, v238, v60
	v_mul_f32_e32 v61, v238, v61
	v_mul_f32_e32 v62, v238, v62
	v_mul_f32_e32 v63, v238, v63
	ds_write_b128 v4, v[60:63] offset:6144
	v_mul_f32_e32 v64, v239, v64
	v_mul_f32_e32 v65, v239, v65
	v_mul_f32_e32 v66, v239, v66
	v_mul_f32_e32 v67, v239, v67
	ds_write_b128 v4, v[64:67] offset:7168
	s_waitcnt lgkmcnt(0)
	s_barrier
; #define GAS __attribute__((address_space(1)))
; #define LAS __attribute__((address_space(3)))
; #define LDS_WAIT() asm volatile("s_waitcnt lgkmcnt(0)" ::: "memory")
;     ...
; #pragma unroll
;     for (int i = 0; i < 32; ++i) v[i] = sc >= 0 ? W[(size_t)(k0 + 2 * i + (lane >> 5)) * Nsrc + sc] : 0.f;
; #pragma unroll
;     for (int i = 0; i < 32; ++i) { const int k = k0 + 2 * i + (lane >> 5); float x = v[i] * wscale; if (KS) x *= (k < ksplit ? ksA[k] : ksB[k - ksplit]); scr[(2 * i + (lane >> 5)) * 33 + (lane & 31)] = x; }
;     LDS_WAIT(); asm volatile("" ::: "memory");
;     const int c = lane & 7;
; #pragma unroll
;     for (int j = 0; j < 4; ++j) { const int n = (lane >> 3) + 8 * j; const LAS float* s = scr + (8 * c) * 33 + n;
;         const unsigned long long o = (unsigned long long)pg8::pk4_fp8(s[0 * 33], s[1 * 33], s[2 * 33], s[3 * 33]) | ((unsigned long long)pg8::pk4_fp8(s[4 * 33], s[5 * 33], s[6 * 33], s[7 * 33]) << 32);
;         *(GAS unsigned long long*)(WT + (size_t)(n0 + n) * K + k0 + 8 * c) = o; }
;     LDS_WAIT(); asm volatile("" ::: "memory");
	s_add_i32 s19, s39, 126
	s_min_u32 s19, s19, 127
	s_lshl_b32 s19, s19, 9
	s_add_u32 s12, s46, s19
	s_addc_u32 s13, s47, 0
	global_load_dwordx4 v[36:39], v30, s[12:13]
	s_add_u32 s12, s12, 0x20000
	s_addc_u32 s13, s13, 0
	global_load_dwordx4 v[40:43], v30, s[12:13]
	s_add_u32 s12, s12, 0x20000
	s_addc_u32 s13, s13, 0
	global_load_dwordx4 v[44:47], v30, s[12:13]
	s_add_u32 s12, s12, 0x20000
	s_addc_u32 s13, s13, 0
	global_load_dwordx4 v[48:51], v30, s[12:13]
	s_add_u32 s12, s12, 0x20000
	s_addc_u32 s13, s13, 0
	global_load_dwordx4 v[52:55], v30, s[12:13]
	s_add_u32 s12, s12, 0x20000
	s_addc_u32 s13, s13, 0
	global_load_dwordx4 v[56:59], v30, s[12:13]
	s_add_u32 s12, s12, 0x20000
	s_addc_u32 s13, s13, 0
	global_load_dwordx4 v[60:63], v30, s[12:13]
	s_add_u32 s12, s12, 0x20000
	s_addc_u32 s13, s13, 0
	global_load_dwordx4 v[64:67], v30, s[12:13]
	s_add_i32 s19, s39, 114
	s_min_u32 s19, s19, 127
	s_lshl_b32 s19, s19, 19
	s_add_u32 s14, s64, s19
	s_addc_u32 s15, s65, 0
	ds_read_b32 v170, v6
	ds_read_b32 v171, v6 offset:512
	ds_read_b32 v172, v6 offset:1024
	ds_read_b32 v173, v6 offset:1536
	ds_read_b32 v174, v6 offset:2048
	ds_read_b32 v175, v6 offset:2560
	ds_read_b32 v176, v6 offset:3072
	ds_read_b32 v177, v6 offset:3584
	ds_read_b32 v196, v6 offset:4096
	ds_read_b32 v197, v6 offset:4608
	ds_read_b32 v198, v6 offset:5120
	ds_read_b32 v199, v6 offset:5632
	ds_read_b32 v200, v6 offset:6144
	ds_read_b32 v201, v6 offset:6656
	ds_read_b32 v202, v6 offset:7168
	ds_read_b32 v203, v6 offset:7680
	s_waitcnt lgkmcnt(0)
	v_max_f32_e32 v170, v170, v170
	v_max_f32_e32 v171, v171, v171
	v_max_f32_e32 v172, v172, v172
	v_max_f32_e32 v173, v173, v173
	v_max_f32_e32 v174, v174, v174
	v_max_f32_e32 v175, v175, v175
	v_max_f32_e32 v176, v176, v176
	v_max_f32_e32 v177, v177, v177
	v_max_f32_e32 v196, v196, v196
	v_max_f32_e32 v197, v197, v197
	v_max_f32_e32 v198, v198, v198
	v_max_f32_e32 v199, v199, v199
	v_max_f32_e32 v200, v200, v200
	v_max_f32_e32 v201, v201, v201
	v_max_f32_e32 v202, v202, v202
	v_max_f32_e32 v203, v203, v203
	v_med3_f32 v170, v170, s20, v13
	v_med3_f32 v171, v171, s20, v13
	v_med3_f32 v172, v172, s20, v13
	v_med3_f32 v173, v173, s20, v13
	v_med3_f32 v174, v174, s20, v13
	v_med3_f32 v175, v175, s20, v13
	v_med3_f32 v176, v176, s20, v13
	v_med3_f32 v177, v177, s20, v13
	v_med3_f32 v196, v196, s20, v13
	v_med3_f32 v197, v197, s20, v13
	v_med3_f32 v198, v198, s20, v13
	v_med3_f32 v199, v199, s20, v13
	v_med3_f32 v200, v200, s20, v13
	v_med3_f32 v201, v201, s20, v13
	v_med3_f32 v202, v202, s20, v13
	v_med3_f32 v203, v203, s20, v13
	v_mov_b32_e32 v208, 0
	v_mov_b32_e32 v209, 0
	v_mov_b32_e32 v210, 0
	v_mov_b32_e32 v211, 0
	v_cvt_pk_fp8_f32 v208, v170, v171
	v_cvt_pk_fp8_f32 v209, v174, v175
	v_cvt_pk_fp8_f32 v210, v196, v197
	v_cvt_pk_fp8_f32 v211, v200, v201
	v_cvt_pk_fp8_f32 v208, v172, v173 op_sel:[0,0,1]
	v_cvt_pk_fp8_f32 v209, v176, v177 op_sel:[0,0,1]
	v_cvt_pk_fp8_f32 v210, v198, v199 op_sel:[0,0,1]
	v_cvt_pk_fp8_f32 v211, v202, v203 op_sel:[0,0,1]
	s_nop 0
	global_store_dwordx4 v28, v[208:211], s[14:15]
	ds_read_b32 v170, v8
	ds_read_b32 v171, v8 offset:512
	ds_read_b32 v172, v8 offset:1024
	ds_read_b32 v173, v8 offset:1536
	ds_read_b32 v174, v8 offset:2048
	ds_read_b32 v175, v8 offset:2560
	ds_read_b32 v176, v8 offset:3072
	ds_read_b32 v177, v8 offset:3584
	ds_read_b32 v196, v8 offset:4096
	ds_read_b32 v197, v8 offset:4608
	ds_read_b32 v198, v8 offset:5120
	ds_read_b32 v199, v8 offset:5632
	ds_read_b32 v200, v8 offset:6144
	ds_read_b32 v201, v8 offset:6656
	ds_read_b32 v202, v8 offset:7168
	ds_read_b32 v203, v8 offset:7680
	s_waitcnt lgkmcnt(0)
	v_max_f32_e32 v170, v170, v170
	v_max_f32_e32 v171, v171, v171
	v_max_f32_e32 v172, v172, v172
	v_max_f32_e32 v173, v173, v173
	v_max_f32_e32 v174, v174, v174
	v_max_f32_e32 v175, v175, v175
	v_max_f32_e32 v176, v176, v176
	v_max_f32_e32 v177, v177, v177
	v_max_f32_e32 v196, v196, v196
	v_max_f32_e32 v197, v197, v197
	v_max_f32_e32 v198, v198, v198
	v_max_f32_e32 v199, v199, v199
	v_max_f32_e32 v200, v200, v200
	v_max_f32_e32 v201, v201, v201
	v_max_f32_e32 v202, v202, v202
	v_max_f32_e32 v203, v203, v203
	v_med3_f32 v170, v170, s20, v13
	v_med3_f32 v171, v171, s20, v13
	v_med3_f32 v172, v172, s20, v13
	v_med3_f32 v173, v173, s20, v13
	v_med3_f32 v174, v174, s20, v13
	v_med3_f32 v175, v175, s20, v13
	v_med3_f32 v176, v176, s20, v13
	v_med3_f32 v177, v177, s20, v13
	v_med3_f32 v196, v196, s20, v13
	v_med3_f32 v197, v197, s20, v13
	v_med3_f32 v198, v198, s20, v13
	v_med3_f32 v199, v199, s20, v13
	v_med3_f32 v200, v200, s20, v13
	v_med3_f32 v201, v201, s20, v13
	v_med3_f32 v202, v202, s20, v13
	v_med3_f32 v203, v203, s20, v13
	v_mov_b32_e32 v208, 0
	v_mov_b32_e32 v209, 0
	v_mov_b32_e32 v210, 0
	v_mov_b32_e32 v211, 0
	v_cvt_pk_fp8_f32 v208, v170, v171
	v_cvt_pk_fp8_f32 v209, v174, v175
	v_cvt_pk_fp8_f32 v210, v196, v197
	v_cvt_pk_fp8_f32 v211, v200, v201
	v_cvt_pk_fp8_f32 v208, v172, v173 op_sel:[0,0,1]
	v_cvt_pk_fp8_f32 v209, v176, v177 op_sel:[0,0,1]
	v_cvt_pk_fp8_f32 v210, v198, v199 op_sel:[0,0,1]
	v_cvt_pk_fp8_f32 v211, v202, v203 op_sel:[0,0,1]
	s_nop 0
	global_store_dwordx4 v29, v[208:211], s[14:15]
	s_waitcnt vmcnt(32)
	v_mul_f32_e32 v68, v232, v68
	v_mul_f32_e32 v69, v232, v69
	v_mul_f32_e32 v70, v232, v70
	v_mul_f32_e32 v71, v232, v71
	ds_write_b128 v5, v[68:71]
	v_mul_f32_e32 v72, v233, v72
	v_mul_f32_e32 v73, v233, v73
	v_mul_f32_e32 v74, v233, v74
	v_mul_f32_e32 v75, v233, v75
	ds_write_b128 v5, v[72:75] offset:1024
	v_mul_f32_e32 v76, v234, v76
	v_mul_f32_e32 v77, v234, v77
	v_mul_f32_e32 v78, v234, v78
	v_mul_f32_e32 v79, v234, v79
	ds_write_b128 v5, v[76:79] offset:2048
	v_mul_f32_e32 v80, v235, v80
	v_mul_f32_e32 v81, v235, v81
	v_mul_f32_e32 v82, v235, v82
	v_mul_f32_e32 v83, v235, v83
	ds_write_b128 v5, v[80:83] offset:3072
	v_mul_f32_e32 v84, v236, v84
	v_mul_f32_e32 v85, v236, v85
	v_mul_f32_e32 v86, v236, v86
	v_mul_f32_e32 v87, v236, v87
	ds_write_b128 v5, v[84:87] offset:4096
	v_mul_f32_e32 v88, v237, v88
	v_mul_f32_e32 v89, v237, v89
	v_mul_f32_e32 v90, v237, v90
	v_mul_f32_e32 v91, v237, v91
	ds_write_b128 v5, v[88:91] offset:5120
	v_mul_f32_e32 v92, v238, v92
	v_mul_f32_e32 v93, v238, v93
	v_mul_f32_e32 v94, v238, v94
	v_mul_f32_e32 v95, v238, v95
	ds_write_b128 v5, v[92:95] offset:6144
	v_mul_f32_e32 v96, v239, v96
	v_mul_f32_e32 v97, v239, v97
	v_mul_f32_e32 v98, v239, v98
	v_mul_f32_e32 v99, v239, v99
	ds_write_b128 v5, v[96:99] offset:7168
	s_waitcnt lgkmcnt(0)
	s_barrier
; #define GAS __attribute__((address_space(1)))
; #define LAS __attribute__((address_space(3)))
; #define LDS_WAIT() asm volatile("s_waitcnt lgkmcnt(0)" ::: "memory")
;     ...
; #pragma unroll
;     for (int i = 0; i < 32; ++i) v[i] = sc >= 0 ? W[(size_t)(k0 + 2 * i + (lane >> 5)) * Nsrc + sc] : 0.f;
; #pragma unroll
;     for (int i = 0; i < 32; ++i) { const int k = k0 + 2 * i + (lane >> 5); float x = v[i] * wscale; if (KS) x *= (k < ksplit ? ksA[k] : ksB[k - ksplit]); scr[(2 * i + (lane >> 5)) * 33 + (lane & 31)] = x; }
;     LDS_WAIT(); asm volatile("" ::: "memory");
;     const int c = lane & 7;
; #pragma unroll
;     for (int j = 0; j < 4; ++j) { const int n = (lane >> 3) + 8 * j; const LAS float* s = scr + (8 * c) * 33 + n;
;         const unsigned long long o = (unsigned long long)pg8::pk4_fp8(s[0 * 33], s[1 * 33], s[2 * 33], s[3 * 33]) | ((unsigned long long)pg8::pk4_fp8(s[4 * 33], s[5 * 33], s[6 * 33], s[7 * 33]) << 32);
;         *(GAS unsigned long long*)(WT + (size_t)(n0 + n) * K + k0 + 8 * c) = o; }
;     LDS_WAIT(); asm volatile("" ::: "memory");
	s_add_i32 s19, s39, 117
	s_min_u32 s19, s19, 127
	s_lshl_b32 s19, s19, 19
	s_add_u32 s14, s64, s19
	s_addc_u32 s15, s65, 0
	ds_read_b32 v170, v7
	ds_read_b32 v171, v7 offset:512
	ds_read_b32 v172, v7 offset:1024
	ds_read_b32 v173, v7 offset:1536
	ds_read_b32 v174, v7 offset:2048
	ds_read_b32 v175, v7 offset:2560
	ds_read_b32 v176, v7 offset:3072
	ds_read_b32 v177, v7 offset:3584
	ds_read_b32 v196, v7 offset:4096
	ds_read_b32 v197, v7 offset:4608
	ds_read_b32 v198, v7 offset:5120
	ds_read_b32 v199, v7 offset:5632
	ds_read_b32 v200, v7 offset:6144
	ds_read_b32 v201, v7 offset:6656
	ds_read_b32 v202, v7 offset:7168
	ds_read_b32 v203, v7 offset:7680
	s_waitcnt lgkmcnt(0)
	v_max_f32_e32 v170, v170, v170
	v_max_f32_e32 v171, v171, v171
	v_max_f32_e32 v172, v172, v172
	v_max_f32_e32 v173, v173, v173
	v_max_f32_e32 v174, v174, v174
	v_max_f32_e32 v175, v175, v175
	v_max_f32_e32 v176, v176, v176
	v_max_f32_e32 v177, v177, v177
	v_max_f32_e32 v196, v196, v196
	v_max_f32_e32 v197, v197, v197
	v_max_f32_e32 v198, v198, v198
	v_max_f32_e32 v199, v199, v199
	v_max_f32_e32 v200, v200, v200
	v_max_f32_e32 v201, v201, v201
	v_max_f32_e32 v202, v202, v202
	v_max_f32_e32 v203, v203, v203
	v_med3_f32 v170, v170, s20, v13
	v_med3_f32 v171, v171, s20, v13
	v_med3_f32 v172, v172, s20, v13
	v_med3_f32 v173, v173, s20, v13
	v_med3_f32 v174, v174, s20, v13
	v_med3_f32 v175, v175, s20, v13
	v_med3_f32 v176, v176, s20, v13
	v_med3_f32 v177, v177, s20, v13
	v_med3_f32 v196, v196, s20, v13
	v_med3_f32 v197, v197, s20, v13
	v_med3_f32 v198, v198, s20, v13
	v_med3_f32 v199, v199, s20, v13
	v_med3_f32 v200, v200, s20, v13
	v_med3_f32 v201, v201, s20, v13
	v_med3_f32 v202, v202, s20, v13
	v_med3_f32 v203, v203, s20, v13
	v_mov_b32_e32 v208, 0
	v_mov_b32_e32 v209, 0
	v_mov_b32_e32 v210, 0
	v_mov_b32_e32 v211, 0
	v_cvt_pk_fp8_f32 v208, v170, v171
	v_cvt_pk_fp8_f32 v209, v174, v175
	v_cvt_pk_fp8_f32 v210, v196, v197
	v_cvt_pk_fp8_f32 v211, v200, v201
	v_cvt_pk_fp8_f32 v208, v172, v173 op_sel:[0,0,1]
	v_cvt_pk_fp8_f32 v209, v176, v177 op_sel:[0,0,1]
	v_cvt_pk_fp8_f32 v210, v198, v199 op_sel:[0,0,1]
	v_cvt_pk_fp8_f32 v211, v202, v203 op_sel:[0,0,1]
	s_nop 0
	global_store_dwordx4 v28, v[208:211], s[14:15]
	ds_read_b32 v170, v9
	ds_read_b32 v171, v9 offset:512
	ds_read_b32 v172, v9 offset:1024
	ds_read_b32 v173, v9 offset:1536
	ds_read_b32 v174, v9 offset:2048
	ds_read_b32 v175, v9 offset:2560
	ds_read_b32 v176, v9 offset:3072
	ds_read_b32 v177, v9 offset:3584
	ds_read_b32 v196, v9 offset:4096
	ds_read_b32 v197, v9 offset:4608
	ds_read_b32 v198, v9 offset:5120
	ds_read_b32 v199, v9 offset:5632
	ds_read_b32 v200, v9 offset:6144
	ds_read_b32 v201, v9 offset:6656
	ds_read_b32 v202, v9 offset:7168
	ds_read_b32 v203, v9 offset:7680
	s_waitcnt lgkmcnt(0)
	v_max_f32_e32 v170, v170, v170
	v_max_f32_e32 v171, v171, v171
	v_max_f32_e32 v172, v172, v172
	v_max_f32_e32 v173, v173, v173
	v_max_f32_e32 v174, v174, v174
	v_max_f32_e32 v175, v175, v175
	v_max_f32_e32 v176, v176, v176
	v_max_f32_e32 v177, v177, v177
	v_max_f32_e32 v196, v196, v196
	v_max_f32_e32 v197, v197, v197
	v_max_f32_e32 v198, v198, v198
	v_max_f32_e32 v199, v199, v199
	v_max_f32_e32 v200, v200, v200
	v_max_f32_e32 v201, v201, v201
	v_max_f32_e32 v202, v202, v202
	v_max_f32_e32 v203, v203, v203
	v_med3_f32 v170, v170, s20, v13
	v_med3_f32 v171, v171, s20, v13
	v_med3_f32 v172, v172, s20, v13
	v_med3_f32 v173, v173, s20, v13
	v_med3_f32 v174, v174, s20, v13
	v_med3_f32 v175, v175, s20, v13
	v_med3_f32 v176, v176, s20, v13
	v_med3_f32 v177, v177, s20, v13
	v_med3_f32 v196, v196, s20, v13
	v_med3_f32 v197, v197, s20, v13
	v_med3_f32 v198, v198, s20, v13
	v_med3_f32 v199, v199, s20, v13
	v_med3_f32 v200, v200, s20, v13
	v_med3_f32 v201, v201, s20, v13
	v_med3_f32 v202, v202, s20, v13
	v_med3_f32 v203, v203, s20, v13
	v_mov_b32_e32 v208, 0
	v_mov_b32_e32 v209, 0
	v_mov_b32_e32 v210, 0
	v_mov_b32_e32 v211, 0
	v_cvt_pk_fp8_f32 v208, v170, v171
	v_cvt_pk_fp8_f32 v209, v174, v175
	v_cvt_pk_fp8_f32 v210, v196, v197
	v_cvt_pk_fp8_f32 v211, v200, v201
	v_cvt_pk_fp8_f32 v208, v172, v173 op_sel:[0,0,1]
	v_cvt_pk_fp8_f32 v209, v176, v177 op_sel:[0,0,1]
	v_cvt_pk_fp8_f32 v210, v198, v199 op_sel:[0,0,1]
	v_cvt_pk_fp8_f32 v211, v202, v203 op_sel:[0,0,1]
	s_nop 0
	global_store_dwordx4 v29, v[208:211], s[14:15]
	s_waitcnt vmcnt(24)
	v_mul_f32_e32 v100, v232, v100
	v_mul_f32_e32 v101, v232, v101
	v_mul_f32_e32 v102, v232, v102
	v_mul_f32_e32 v103, v232, v103
	ds_write_b128 v4, v[100:103]
	v_mul_f32_e32 v104, v233, v104
	v_mul_f32_e32 v105, v233, v105
	v_mul_f32_e32 v106, v233, v106
	v_mul_f32_e32 v107, v233, v107
	ds_write_b128 v4, v[104:107] offset:1024
	v_mul_f32_e32 v108, v234, v108
	v_mul_f32_e32 v109, v234, v109
	v_mul_f32_e32 v110, v234, v110
	v_mul_f32_e32 v111, v234, v111
	ds_write_b128 v4, v[108:111] offset:2048
	v_mul_f32_e32 v112, v235, v112
	v_mul_f32_e32 v113, v235, v113
	v_mul_f32_e32 v114, v235, v114
	v_mul_f32_e32 v115, v235, v115
	ds_write_b128 v4, v[112:115] offset:3072
	v_mul_f32_e32 v116, v236, v116
	v_mul_f32_e32 v117, v236, v117
	v_mul_f32_e32 v118, v236, v118
	v_mul_f32_e32 v119, v236, v119
	ds_write_b128 v4, v[116:119] offset:4096
	v_mul_f32_e32 v120, v237, v120
	v_mul_f32_e32 v121, v237, v121
	v_mul_f32_e32 v122, v237, v122
	v_mul_f32_e32 v123, v237, v123
	ds_write_b128 v4, v[120:123] offset:5120
	v_mul_f32_e32 v124, v238, v124
	v_mul_f32_e32 v125, v238, v125
	v_mul_f32_e32 v126, v238, v126
	v_mul_f32_e32 v127, v238, v127
	ds_write_b128 v4, v[124:127] offset:6144
	v_mul_f32_e32 v128, v239, v128
	v_mul_f32_e32 v129, v239, v129
	v_mul_f32_e32 v130, v239, v130
	v_mul_f32_e32 v131, v239, v131
	ds_write_b128 v4, v[128:131] offset:7168
	s_waitcnt lgkmcnt(0)
	s_barrier
; #define GAS __attribute__((address_space(1)))
; #define LAS __attribute__((address_space(3)))
; #define LDS_WAIT() asm volatile("s_waitcnt lgkmcnt(0)" ::: "memory")
;     ...
; #pragma unroll
;     for (int i = 0; i < 32; ++i) v[i] = sc >= 0 ? W[(size_t)(k0 + 2 * i + (lane >> 5)) * Nsrc + sc] : 0.f;
; #pragma unroll
;     for (int i = 0; i < 32; ++i) { const int k = k0 + 2 * i + (lane >> 5); float x = v[i] * wscale; if (KS) x *= (k < ksplit ? ksA[k] : ksB[k - ksplit]); scr[(2 * i + (lane >> 5)) * 33 + (lane & 31)] = x; }
;     LDS_WAIT(); asm volatile("" ::: "memory");
;     const int c = lane & 7;
; #pragma unroll
;     for (int j = 0; j < 4; ++j) { const int n = (lane >> 3) + 8 * j; const LAS float* s = scr + (8 * c) * 33 + n;
;         const unsigned long long o = (unsigned long long)pg8::pk4_fp8(s[0 * 33], s[1 * 33], s[2 * 33], s[3 * 33]) | ((unsigned long long)pg8::pk4_fp8(s[4 * 33], s[5 * 33], s[6 * 33], s[7 * 33]) << 32);
;         *(GAS unsigned long long*)(WT + (size_t)(n0 + n) * K + k0 + 8 * c) = o; }
;     LDS_WAIT(); asm volatile("" ::: "memory");
	s_add_i32 s19, s39, 120
	s_min_u32 s19, s19, 127
	s_lshl_b32 s19, s19, 19
	s_add_u32 s14, s64, s19
	s_addc_u32 s15, s65, 0
	ds_read_b32 v170, v6
	ds_read_b32 v171, v6 offset:512
	ds_read_b32 v172, v6 offset:1024
	ds_read_b32 v173, v6 offset:1536
	ds_read_b32 v174, v6 offset:2048
	ds_read_b32 v175, v6 offset:2560
	ds_read_b32 v176, v6 offset:3072
	ds_read_b32 v177, v6 offset:3584
	ds_read_b32 v196, v6 offset:4096
	ds_read_b32 v197, v6 offset:4608
	ds_read_b32 v198, v6 offset:5120
	ds_read_b32 v199, v6 offset:5632
	ds_read_b32 v200, v6 offset:6144
	ds_read_b32 v201, v6 offset:6656
	ds_read_b32 v202, v6 offset:7168
	ds_read_b32 v203, v6 offset:7680
	s_waitcnt lgkmcnt(0)
	v_max_f32_e32 v170, v170, v170
	v_max_f32_e32 v171, v171, v171
	v_max_f32_e32 v172, v172, v172
	v_max_f32_e32 v173, v173, v173
	v_max_f32_e32 v174, v174, v174
	v_max_f32_e32 v175, v175, v175
	v_max_f32_e32 v176, v176, v176
	v_max_f32_e32 v177, v177, v177
	v_max_f32_e32 v196, v196, v196
	v_max_f32_e32 v197, v197, v197
	v_max_f32_e32 v198, v198, v198
	v_max_f32_e32 v199, v199, v199
	v_max_f32_e32 v200, v200, v200
	v_max_f32_e32 v201, v201, v201
	v_max_f32_e32 v202, v202, v202
	v_max_f32_e32 v203, v203, v203
	v_med3_f32 v170, v170, s20, v13
	v_med3_f32 v171, v171, s20, v13
	v_med3_f32 v172, v172, s20, v13
	v_med3_f32 v173, v173, s20, v13
	v_med3_f32 v174, v174, s20, v13
	v_med3_f32 v175, v175, s20, v13
	v_med3_f32 v176, v176, s20, v13
	v_med3_f32 v177, v177, s20, v13
	v_med3_f32 v196, v196, s20, v13
	v_med3_f32 v197, v197, s20, v13
	v_med3_f32 v198, v198, s20, v13
	v_med3_f32 v199, v199, s20, v13
	v_med3_f32 v200, v200, s20, v13
	v_med3_f32 v201, v201, s20, v13
	v_med3_f32 v202, v202, s20, v13
	v_med3_f32 v203, v203, s20, v13
	v_mov_b32_e32 v208, 0
	v_mov_b32_e32 v209, 0
	v_mov_b32_e32 v210, 0
	v_mov_b32_e32 v211, 0
	v_cvt_pk_fp8_f32 v208, v170, v171
	v_cvt_pk_fp8_f32 v209, v174, v175
	v_cvt_pk_fp8_f32 v210, v196, v197
	v_cvt_pk_fp8_f32 v211, v200, v201
	v_cvt_pk_fp8_f32 v208, v172, v173 op_sel:[0,0,1]
	v_cvt_pk_fp8_f32 v209, v176, v177 op_sel:[0,0,1]
	v_cvt_pk_fp8_f32 v210, v198, v199 op_sel:[0,0,1]
	v_cvt_pk_fp8_f32 v211, v202, v203 op_sel:[0,0,1]
	s_nop 0
	global_store_dwordx4 v28, v[208:211], s[14:15]
	ds_read_b32 v170, v8
	ds_read_b32 v171, v8 offset:512
	ds_read_b32 v172, v8 offset:1024
	ds_read_b32 v173, v8 offset:1536
	ds_read_b32 v174, v8 offset:2048
	ds_read_b32 v175, v8 offset:2560
	ds_read_b32 v176, v8 offset:3072
	ds_read_b32 v177, v8 offset:3584
	ds_read_b32 v196, v8 offset:4096
	ds_read_b32 v197, v8 offset:4608
	ds_read_b32 v198, v8 offset:5120
	ds_read_b32 v199, v8 offset:5632
	ds_read_b32 v200, v8 offset:6144
	ds_read_b32 v201, v8 offset:6656
	ds_read_b32 v202, v8 offset:7168
	ds_read_b32 v203, v8 offset:7680
	s_waitcnt lgkmcnt(0)
	v_max_f32_e32 v170, v170, v170
	v_max_f32_e32 v171, v171, v171
	v_max_f32_e32 v172, v172, v172
	v_max_f32_e32 v173, v173, v173
	v_max_f32_e32 v174, v174, v174
	v_max_f32_e32 v175, v175, v175
	v_max_f32_e32 v176, v176, v176
	v_max_f32_e32 v177, v177, v177
	v_max_f32_e32 v196, v196, v196
	v_max_f32_e32 v197, v197, v197
	v_max_f32_e32 v198, v198, v198
	v_max_f32_e32 v199, v199, v199
	v_max_f32_e32 v200, v200, v200
	v_max_f32_e32 v201, v201, v201
	v_max_f32_e32 v202, v202, v202
	v_max_f32_e32 v203, v203, v203
	v_med3_f32 v170, v170, s20, v13
	v_med3_f32 v171, v171, s20, v13
	v_med3_f32 v172, v172, s20, v13
	v_med3_f32 v173, v173, s20, v13
	v_med3_f32 v174, v174, s20, v13
	v_med3_f32 v175, v175, s20, v13
	v_med3_f32 v176, v176, s20, v13
	v_med3_f32 v177, v177, s20, v13
	v_med3_f32 v196, v196, s20, v13
	v_med3_f32 v197, v197, s20, v13
	v_med3_f32 v198, v198, s20, v13
	v_med3_f32 v199, v199, s20, v13
	v_med3_f32 v200, v200, s20, v13
	v_med3_f32 v201, v201, s20, v13
	v_med3_f32 v202, v202, s20, v13
	v_med3_f32 v203, v203, s20, v13
	v_mov_b32_e32 v208, 0
	v_mov_b32_e32 v209, 0
	v_mov_b32_e32 v210, 0
	v_mov_b32_e32 v211, 0
	v_cvt_pk_fp8_f32 v208, v170, v171
	v_cvt_pk_fp8_f32 v209, v174, v175
	v_cvt_pk_fp8_f32 v210, v196, v197
	v_cvt_pk_fp8_f32 v211, v200, v201
	v_cvt_pk_fp8_f32 v208, v172, v173 op_sel:[0,0,1]
	v_cvt_pk_fp8_f32 v209, v176, v177 op_sel:[0,0,1]
	v_cvt_pk_fp8_f32 v210, v198, v199 op_sel:[0,0,1]
	v_cvt_pk_fp8_f32 v211, v202, v203 op_sel:[0,0,1]
	s_nop 0
	global_store_dwordx4 v29, v[208:211], s[14:15]
	s_waitcnt vmcnt(16)
	v_mul_f32_e32 v132, v232, v132
	v_mul_f32_e32 v133, v232, v133
	v_mul_f32_e32 v134, v232, v134
	v_mul_f32_e32 v135, v232, v135
	ds_write_b128 v5, v[132:135]
	v_mul_f32_e32 v136, v233, v136
	v_mul_f32_e32 v137, v233, v137
	v_mul_f32_e32 v138, v233, v138
	v_mul_f32_e32 v139, v233, v139
	ds_write_b128 v5, v[136:139] offset:1024
	v_mul_f32_e32 v140, v234, v140
	v_mul_f32_e32 v141, v234, v141
	v_mul_f32_e32 v142, v234, v142
	v_mul_f32_e32 v143, v234, v143
	ds_write_b128 v5, v[140:143] offset:2048
	v_mul_f32_e32 v144, v235, v144
	v_mul_f32_e32 v145, v235, v145
	v_mul_f32_e32 v146, v235, v146
	v_mul_f32_e32 v147, v235, v147
	ds_write_b128 v5, v[144:147] offset:3072
	v_mul_f32_e32 v148, v236, v148
	v_mul_f32_e32 v149, v236, v149
	v_mul_f32_e32 v150, v236, v150
	v_mul_f32_e32 v151, v236, v151
	ds_write_b128 v5, v[148:151] offset:4096
	v_mul_f32_e32 v152, v237, v152
	v_mul_f32_e32 v153, v237, v153
	v_mul_f32_e32 v154, v237, v154
	v_mul_f32_e32 v155, v237, v155
	ds_write_b128 v5, v[152:155] offset:5120
	v_mul_f32_e32 v156, v238, v156
	v_mul_f32_e32 v157, v238, v157
	v_mul_f32_e32 v158, v238, v158
	v_mul_f32_e32 v159, v238, v159
	ds_write_b128 v5, v[156:159] offset:6144
	v_mul_f32_e32 v160, v239, v160
	v_mul_f32_e32 v161, v239, v161
	v_mul_f32_e32 v162, v239, v162
	v_mul_f32_e32 v163, v239, v163
	ds_write_b128 v5, v[160:163] offset:7168
	s_waitcnt lgkmcnt(0)
	s_barrier
; #define GAS __attribute__((address_space(1)))
; #define LAS __attribute__((address_space(3)))
; #define LDS_WAIT() asm volatile("s_waitcnt lgkmcnt(0)" ::: "memory")
;     ...
; #pragma unroll
;     for (int i = 0; i < 32; ++i) v[i] = sc >= 0 ? W[(size_t)(k0 + 2 * i + (lane >> 5)) * Nsrc + sc] : 0.f;
; #pragma unroll
;     for (int i = 0; i < 32; ++i) { const int k = k0 + 2 * i + (lane >> 5); float x = v[i] * wscale; if (KS) x *= (k < ksplit ? ksA[k] : ksB[k - ksplit]); scr[(2 * i + (lane >> 5)) * 33 + (lane & 31)] = x; }
;     LDS_WAIT(); asm volatile("" ::: "memory");
;     const int c = lane & 7;
; #pragma unroll
;     for (int j = 0; j < 4; ++j) { const int n = (lane >> 3) + 8 * j; const LAS float* s = scr + (8 * c) * 33 + n;
;         const unsigned long long o = (unsigned long long)pg8::pk4_fp8(s[0 * 33], s[1 * 33], s[2 * 33], s[3 * 33]) | ((unsigned long long)pg8::pk4_fp8(s[4 * 33], s[5 * 33], s[6 * 33], s[7 * 33]) << 32);
;         *(GAS unsigned long long*)(WT + (size_t)(n0 + n) * K + k0 + 8 * c) = o; }
;     LDS_WAIT(); asm volatile("" ::: "memory");
	s_add_i32 s19, s39, 123
	s_min_u32 s19, s19, 127
	s_lshl_b32 s19, s19, 19
	s_add_u32 s14, s64, s19
	s_addc_u32 s15, s65, 0
	ds_read_b32 v170, v7
	ds_read_b32 v171, v7 offset:512
	ds_read_b32 v172, v7 offset:1024
	ds_read_b32 v173, v7 offset:1536
	ds_read_b32 v174, v7 offset:2048
	ds_read_b32 v175, v7 offset:2560
	ds_read_b32 v176, v7 offset:3072
	ds_read_b32 v177, v7 offset:3584
	ds_read_b32 v196, v7 offset:4096
	ds_read_b32 v197, v7 offset:4608
	ds_read_b32 v198, v7 offset:5120
	ds_read_b32 v199, v7 offset:5632
	ds_read_b32 v200, v7 offset:6144
	ds_read_b32 v201, v7 offset:6656
	ds_read_b32 v202, v7 offset:7168
	ds_read_b32 v203, v7 offset:7680
	s_waitcnt lgkmcnt(0)
	v_max_f32_e32 v170, v170, v170
	v_max_f32_e32 v171, v171, v171
	v_max_f32_e32 v172, v172, v172
	v_max_f32_e32 v173, v173, v173
	v_max_f32_e32 v174, v174, v174
	v_max_f32_e32 v175, v175, v175
	v_max_f32_e32 v176, v176, v176
	v_max_f32_e32 v177, v177, v177
	v_max_f32_e32 v196, v196, v196
	v_max_f32_e32 v197, v197, v197
	v_max_f32_e32 v198, v198, v198
	v_max_f32_e32 v199, v199, v199
	v_max_f32_e32 v200, v200, v200
	v_max_f32_e32 v201, v201, v201
	v_max_f32_e32 v202, v202, v202
	v_max_f32_e32 v203, v203, v203
	v_med3_f32 v170, v170, s20, v13
	v_med3_f32 v171, v171, s20, v13
	v_med3_f32 v172, v172, s20, v13
	v_med3_f32 v173, v173, s20, v13
	v_med3_f32 v174, v174, s20, v13
	v_med3_f32 v175, v175, s20, v13
	v_med3_f32 v176, v176, s20, v13
	v_med3_f32 v177, v177, s20, v13
	v_med3_f32 v196, v196, s20, v13
	v_med3_f32 v197, v197, s20, v13
	v_med3_f32 v198, v198, s20, v13
	v_med3_f32 v199, v199, s20, v13
	v_med3_f32 v200, v200, s20, v13
	v_med3_f32 v201, v201, s20, v13
	v_med3_f32 v202, v202, s20, v13
	v_med3_f32 v203, v203, s20, v13
	v_mov_b32_e32 v208, 0
	v_mov_b32_e32 v209, 0
	v_mov_b32_e32 v210, 0
	v_mov_b32_e32 v211, 0
	v_cvt_pk_fp8_f32 v208, v170, v171
	v_cvt_pk_fp8_f32 v209, v174, v175
	v_cvt_pk_fp8_f32 v210, v196, v197
	v_cvt_pk_fp8_f32 v211, v200, v201
	v_cvt_pk_fp8_f32 v208, v172, v173 op_sel:[0,0,1]
	v_cvt_pk_fp8_f32 v209, v176, v177 op_sel:[0,0,1]
	v_cvt_pk_fp8_f32 v210, v198, v199 op_sel:[0,0,1]
	v_cvt_pk_fp8_f32 v211, v202, v203 op_sel:[0,0,1]
	s_nop 0
	global_store_dwordx4 v28, v[208:211], s[14:15]
	ds_read_b32 v170, v9
	ds_read_b32 v171, v9 offset:512
	ds_read_b32 v172, v9 offset:1024
	ds_read_b32 v173, v9 offset:1536
	ds_read_b32 v174, v9 offset:2048
	ds_read_b32 v175, v9 offset:2560
	ds_read_b32 v176, v9 offset:3072
	ds_read_b32 v177, v9 offset:3584
	ds_read_b32 v196, v9 offset:4096
	ds_read_b32 v197, v9 offset:4608
	ds_read_b32 v198, v9 offset:5120
	ds_read_b32 v199, v9 offset:5632
	ds_read_b32 v200, v9 offset:6144
	ds_read_b32 v201, v9 offset:6656
	ds_read_b32 v202, v9 offset:7168
	ds_read_b32 v203, v9 offset:7680
	s_waitcnt lgkmcnt(0)
	v_max_f32_e32 v170, v170, v170
	v_max_f32_e32 v171, v171, v171
	v_max_f32_e32 v172, v172, v172
	v_max_f32_e32 v173, v173, v173
	v_max_f32_e32 v174, v174, v174
	v_max_f32_e32 v175, v175, v175
	v_max_f32_e32 v176, v176, v176
	v_max_f32_e32 v177, v177, v177
	v_max_f32_e32 v196, v196, v196
	v_max_f32_e32 v197, v197, v197
	v_max_f32_e32 v198, v198, v198
	v_max_f32_e32 v199, v199, v199
	v_max_f32_e32 v200, v200, v200
	v_max_f32_e32 v201, v201, v201
	v_max_f32_e32 v202, v202, v202
	v_max_f32_e32 v203, v203, v203
	v_med3_f32 v170, v170, s20, v13
	v_med3_f32 v171, v171, s20, v13
	v_med3_f32 v172, v172, s20, v13
	v_med3_f32 v173, v173, s20, v13
	v_med3_f32 v174, v174, s20, v13
	v_med3_f32 v175, v175, s20, v13
	v_med3_f32 v176, v176, s20, v13
	v_med3_f32 v177, v177, s20, v13
	v_med3_f32 v196, v196, s20, v13
	v_med3_f32 v197, v197, s20, v13
	v_med3_f32 v198, v198, s20, v13
	v_med3_f32 v199, v199, s20, v13
	v_med3_f32 v200, v200, s20, v13
	v_med3_f32 v201, v201, s20, v13
	v_med3_f32 v202, v202, s20, v13
	v_med3_f32 v203, v203, s20, v13
	v_mov_b32_e32 v208, 0
	v_mov_b32_e32 v209, 0
	v_mov_b32_e32 v210, 0
	v_mov_b32_e32 v211, 0
	v_cvt_pk_fp8_f32 v208, v170, v171
	v_cvt_pk_fp8_f32 v209, v174, v175
	v_cvt_pk_fp8_f32 v210, v196, v197
	v_cvt_pk_fp8_f32 v211, v200, v201
	v_cvt_pk_fp8_f32 v208, v172, v173 op_sel:[0,0,1]
	v_cvt_pk_fp8_f32 v209, v176, v177 op_sel:[0,0,1]
	v_cvt_pk_fp8_f32 v210, v198, v199 op_sel:[0,0,1]
	v_cvt_pk_fp8_f32 v211, v202, v203 op_sel:[0,0,1]
	s_nop 0
	global_store_dwordx4 v29, v[208:211], s[14:15]
	s_waitcnt vmcnt(8)
	v_mul_f32_e32 v36, v232, v36
	v_mul_f32_e32 v37, v232, v37
	v_mul_f32_e32 v38, v232, v38
	v_mul_f32_e32 v39, v232, v39
	ds_write_b128 v4, v[36:39]
	v_mul_f32_e32 v40, v233, v40
	v_mul_f32_e32 v41, v233, v41
	v_mul_f32_e32 v42, v233, v42
	v_mul_f32_e32 v43, v233, v43
	ds_write_b128 v4, v[40:43] offset:1024
	v_mul_f32_e32 v44, v234, v44
	v_mul_f32_e32 v45, v234, v45
	v_mul_f32_e32 v46, v234, v46
	v_mul_f32_e32 v47, v234, v47
	ds_write_b128 v4, v[44:47] offset:2048
	v_mul_f32_e32 v48, v235, v48
	v_mul_f32_e32 v49, v235, v49
	v_mul_f32_e32 v50, v235, v50
	v_mul_f32_e32 v51, v235, v51
	ds_write_b128 v4, v[48:51] offset:3072
	v_mul_f32_e32 v52, v236, v52
	v_mul_f32_e32 v53, v236, v53
	v_mul_f32_e32 v54, v236, v54
	v_mul_f32_e32 v55, v236, v55
	ds_write_b128 v4, v[52:55] offset:4096
	v_mul_f32_e32 v56, v237, v56
	v_mul_f32_e32 v57, v237, v57
	v_mul_f32_e32 v58, v237, v58
	v_mul_f32_e32 v59, v237, v59
	ds_write_b128 v4, v[56:59] offset:5120
	v_mul_f32_e32 v60, v238, v60
	v_mul_f32_e32 v61, v238, v61
	v_mul_f32_e32 v62, v238, v62
	v_mul_f32_e32 v63, v238, v63
	ds_write_b128 v4, v[60:63] offset:6144
	v_mul_f32_e32 v64, v239, v64
	v_mul_f32_e32 v65, v239, v65
	v_mul_f32_e32 v66, v239, v66
	v_mul_f32_e32 v67, v239, v67
	ds_write_b128 v4, v[64:67] offset:7168
	s_waitcnt lgkmcnt(0)
	s_barrier
; #define GAS __attribute__((address_space(1)))
; #define LAS __attribute__((address_space(3)))
; #define LDS_WAIT() asm volatile("s_waitcnt lgkmcnt(0)" ::: "memory")
;     ...
; #pragma unroll
;     for (int i = 0; i < 32; ++i) v[i] = sc >= 0 ? W[(size_t)(k0 + 2 * i + (lane >> 5)) * Nsrc + sc] : 0.f;
; #pragma unroll
;     for (int i = 0; i < 32; ++i) { const int k = k0 + 2 * i + (lane >> 5); float x = v[i] * wscale; if (KS) x *= (k < ksplit ? ksA[k] : ksB[k - ksplit]); scr[(2 * i + (lane >> 5)) * 33 + (lane & 31)] = x; }
;     LDS_WAIT(); asm volatile("" ::: "memory");
;     const int c = lane & 7;
; #pragma unroll
;     for (int j = 0; j < 4; ++j) { const int n = (lane >> 3) + 8 * j; const LAS float* s = scr + (8 * c) * 33 + n;
;         const unsigned long long o = (unsigned long long)pg8::pk4_fp8(s[0 * 33], s[1 * 33], s[2 * 33], s[3 * 33]) | ((unsigned long long)pg8::pk4_fp8(s[4 * 33], s[5 * 33], s[6 * 33], s[7 * 33]) << 32);
;         *(GAS unsigned long long*)(WT + (size_t)(n0 + n) * K + k0 + 8 * c) = o; }
;     LDS_WAIT(); asm volatile("" ::: "memory");
	s_add_i32 s19, s39, 126
	s_min_u32 s19, s19, 127
	s_lshl_b32 s19, s19, 19
	s_add_u32 s14, s64, s19
	s_addc_u32 s15, s65, 0
	ds_read_b32 v170, v6
	ds_read_b32 v171, v6 offset:512
	ds_read_b32 v172, v6 offset:1024
	ds_read_b32 v173, v6 offset:1536
	ds_read_b32 v174, v6 offset:2048
	ds_read_b32 v175, v6 offset:2560
	ds_read_b32 v176, v6 offset:3072
	ds_read_b32 v177, v6 offset:3584
	ds_read_b32 v196, v6 offset:4096
	ds_read_b32 v197, v6 offset:4608
	ds_read_b32 v198, v6 offset:5120
	ds_read_b32 v199, v6 offset:5632
	ds_read_b32 v200, v6 offset:6144
	ds_read_b32 v201, v6 offset:6656
	ds_read_b32 v202, v6 offset:7168
	ds_read_b32 v203, v6 offset:7680
	s_waitcnt lgkmcnt(0)
	v_max_f32_e32 v170, v170, v170
	v_max_f32_e32 v171, v171, v171
	v_max_f32_e32 v172, v172, v172
	v_max_f32_e32 v173, v173, v173
	v_max_f32_e32 v174, v174, v174
	v_max_f32_e32 v175, v175, v175
	v_max_f32_e32 v176, v176, v176
	v_max_f32_e32 v177, v177, v177
	v_max_f32_e32 v196, v196, v196
	v_max_f32_e32 v197, v197, v197
	v_max_f32_e32 v198, v198, v198
	v_max_f32_e32 v199, v199, v199
	v_max_f32_e32 v200, v200, v200
	v_max_f32_e32 v201, v201, v201
	v_max_f32_e32 v202, v202, v202
	v_max_f32_e32 v203, v203, v203
	v_med3_f32 v170, v170, s20, v13
	v_med3_f32 v171, v171, s20, v13
	v_med3_f32 v172, v172, s20, v13
	v_med3_f32 v173, v173, s20, v13
	v_med3_f32 v174, v174, s20, v13
	v_med3_f32 v175, v175, s20, v13
	v_med3_f32 v176, v176, s20, v13
	v_med3_f32 v177, v177, s20, v13
	v_med3_f32 v196, v196, s20, v13
	v_med3_f32 v197, v197, s20, v13
	v_med3_f32 v198, v198, s20, v13
	v_med3_f32 v199, v199, s20, v13
	v_med3_f32 v200, v200, s20, v13
	v_med3_f32 v201, v201, s20, v13
	v_med3_f32 v202, v202, s20, v13
	v_med3_f32 v203, v203, s20, v13
	v_mov_b32_e32 v208, 0
	v_mov_b32_e32 v209, 0
	v_mov_b32_e32 v210, 0
	v_mov_b32_e32 v211, 0
	v_cvt_pk_fp8_f32 v208, v170, v171
	v_cvt_pk_fp8_f32 v209, v174, v175
	v_cvt_pk_fp8_f32 v210, v196, v197
	v_cvt_pk_fp8_f32 v211, v200, v201
	v_cvt_pk_fp8_f32 v208, v172, v173 op_sel:[0,0,1]
	v_cvt_pk_fp8_f32 v209, v176, v177 op_sel:[0,0,1]
	v_cvt_pk_fp8_f32 v210, v198, v199 op_sel:[0,0,1]
	v_cvt_pk_fp8_f32 v211, v202, v203 op_sel:[0,0,1]
	s_nop 0
	global_store_dwordx4 v28, v[208:211], s[14:15]
	ds_read_b32 v170, v8
	ds_read_b32 v171, v8 offset:512
	ds_read_b32 v172, v8 offset:1024
	ds_read_b32 v173, v8 offset:1536
	ds_read_b32 v174, v8 offset:2048
	ds_read_b32 v175, v8 offset:2560
	ds_read_b32 v176, v8 offset:3072
	ds_read_b32 v177, v8 offset:3584
	ds_read_b32 v196, v8 offset:4096
	ds_read_b32 v197, v8 offset:4608
	ds_read_b32 v198, v8 offset:5120
	ds_read_b32 v199, v8 offset:5632
	ds_read_b32 v200, v8 offset:6144
	ds_read_b32 v201, v8 offset:6656
	ds_read_b32 v202, v8 offset:7168
	ds_read_b32 v203, v8 offset:7680
	s_waitcnt lgkmcnt(0)
	v_max_f32_e32 v170, v170, v170
	v_max_f32_e32 v171, v171, v171
	v_max_f32_e32 v172, v172, v172
	v_max_f32_e32 v173, v173, v173
	v_max_f32_e32 v174, v174, v174
	v_max_f32_e32 v175, v175, v175
	v_max_f32_e32 v176, v176, v176
	v_max_f32_e32 v177, v177, v177
	v_max_f32_e32 v196, v196, v196
	v_max_f32_e32 v197, v197, v197
	v_max_f32_e32 v198, v198, v198
	v_max_f32_e32 v199, v199, v199
	v_max_f32_e32 v200, v200, v200
	v_max_f32_e32 v201, v201, v201
	v_max_f32_e32 v202, v202, v202
	v_max_f32_e32 v203, v203, v203
	v_med3_f32 v170, v170, s20, v13
	v_med3_f32 v171, v171, s20, v13
	v_med3_f32 v172, v172, s20, v13
	v_med3_f32 v173, v173, s20, v13
	v_med3_f32 v174, v174, s20, v13
	v_med3_f32 v175, v175, s20, v13
	v_med3_f32 v176, v176, s20, v13
	v_med3_f32 v177, v177, s20, v13
	v_med3_f32 v196, v196, s20, v13
	v_med3_f32 v197, v197, s20, v13
	v_med3_f32 v198, v198, s20, v13
	v_med3_f32 v199, v199, s20, v13
	v_med3_f32 v200, v200, s20, v13
	v_med3_f32 v201, v201, s20, v13
	v_med3_f32 v202, v202, s20, v13
	v_med3_f32 v203, v203, s20, v13
	v_mov_b32_e32 v208, 0
	v_mov_b32_e32 v209, 0
	v_mov_b32_e32 v210, 0
	v_mov_b32_e32 v211, 0
	v_cvt_pk_fp8_f32 v208, v170, v171
	v_cvt_pk_fp8_f32 v209, v174, v175
	v_cvt_pk_fp8_f32 v210, v196, v197
	v_cvt_pk_fp8_f32 v211, v200, v201
	v_cvt_pk_fp8_f32 v208, v172, v173 op_sel:[0,0,1]
	v_cvt_pk_fp8_f32 v209, v176, v177 op_sel:[0,0,1]
	v_cvt_pk_fp8_f32 v210, v198, v199 op_sel:[0,0,1]
	v_cvt_pk_fp8_f32 v211, v202, v203 op_sel:[0,0,1]
	s_nop 0
	global_store_dwordx4 v29, v[208:211], s[14:15]
	s_waitcnt vmcnt(0) lgkmcnt(0)
	s_barrier
